# NA: one-chunk-ahead cache-line touch loads after each stage's K/V loads, vmcnt waits recomputed (on top of NA bias-read hoist + L0 epilogue pipelining)
# baseline (speedup 1.0000x reference)
; template <bool LOCAL>
; __device__ __forceinline__ void na_unit(const bf16* P, const bf16* VT, bf16* YCAT, const LAS float* rpb_l, LAS bf16* buf, int b, int gr, int hp, int qblk, int tid) {
;     ...
;     v4u ld[2][2];
;     const int lrow = (tid >> 3) & 63, lseg = tid & 7;
;     ...
;     bf16x8 qf[2];
; #pragma unroll
;     for (int ks = 0; ks < 2; ++ks) qf[ks] = *(const bf16x8*)(P + (size_t)(qrow0 + fr) * DINP + h * 64 + 32 * ks + 8 * fq);
;     f32x4 sl[16], sc[16];
;     float m = -1.0e30f, lsum = 0.f;
;     f32x4 o[4];
; #pragma unroll
;     for (int dt = 0; dt < 4; ++dt) o[dt] = (f32x4){0.f, 0.f, 0.f, 0.f};
;     NA_ISSUE(0); NA_ISSUE(1); NA_STORE(0);
;     __syncthreads();
; #pragma unroll
;     for (int sidx = 0; sidx < 2 * NCH; ++sidx) {
;         if (sidx + 2 < 2 * NCH) NA_ISSUE(sidx + 2);
;         const LAS bf16* cb = buf + (sidx & 1) * 9216 + hh * 4608;
;         if (sidx < NCH) {
;             const int c = sidx;
;             if (LOCAL && c < 8) {
; #pragma unroll
;                 for (int t2 = 0; t2 < 2; ++t2) {
;                     const LAS bf16* kp = cb + (kc0 + 16 * t2 + fr) * 72 + 8 * fq;
;                     f32x4 acc = {0.f, 0.f, 0.f, 0.f};
;                     acc = __builtin_amdgcn_mfma_f32_16x16x32_bf16(*(const LAS bf16x8*)(kp), qf[0], acc, 0, 0, 0);
;                     acc = __builtin_amdgcn_mfma_f32_16x16x32_bf16(*(const LAS bf16x8*)(kp + 32), qf[1], acc, 0, 0, 0);
;                     const LAS float* rb = rpb + (r0 + c - gr + 7) * 31 + 15 - qcol;
; #pragma unroll
;                     for (int e = 0; e < 4; ++e) { const int kcol = kc0 + 16 * t2 + 4 * fq + e; const bool ok = (kcol >= cs) && (kcol < cs + 16);
;                         const float sv = ok ? acc[e] * 0.125f + rb[ok ? kcol : qcol] : -1.0e30f; acc[e] = sv; m = fmaxf(m, sv); }
;                     sl[2 * (c < 8 ? c : 0) + t2] = acc; }
;             } else {
;                 const int cc = c - NLOC;
; #pragma unroll
;                 for (int t4 = 0; t4 < 4; ++t4) {
;                     const LAS bf16* kp = cb + (16 * t4 + fr) * 72 + 8 * fq;
;                     f32x4 acc = {0.f, 0.f, 0.f, 0.f};
;                     acc = __builtin_amdgcn_mfma_f32_16x16x32_bf16(*(const LAS bf16x8*)(kp), qf[0], acc, 0, 0, 0);
;                     acc = __builtin_amdgcn_mfma_f32_16x16x32_bf16(*(const LAS bf16x8*)(kp + 32), qf[1], acc, 0, 0, 0);
; #pragma unroll
.LBB0_397:
	v_mov_b32_e32 v94, v0
	s_movk_i32 s2, 0x2400
	v_and_b32_e32 v90, 15, v94
	v_bfe_u32 v92, v94, 4, 2
	v_ashrrev_i32_e32 v93, 8, v94
	s_mov_b64 s[0:1], -1
	s_cmpk_gt_i32 s76, 0x7ff
	v_bfe_u32 v89, v94, 3, 6
	v_lshlrev_b32_e32 v76, 3, v92
	v_lshlrev_b32_e32 v70, 4, v92
	v_mad_i32_i24 v87, v93, s2, 0
	v_mul_u32_u24_e32 v88, 0x90, v90
	s_waitcnt lgkmcnt(0)
	s_barrier
	s_cbranch_scc0 .LBB0_399
	s_lshl_b32 s0, s76, 4
	s_and_b32 s0, s0, 0xffffff00
	s_addk_i32 s0, 0x8000
	v_mov_b64_e32 v[78:79], s[8:9]
	s_lshl_b32 s1, s76, 5
	v_or_b32_e32 v77, s0, v89
	v_lshlrev_b32_e32 v4, 4, v94
	s_and_b32 s16, s1, 0x180
	v_mad_u64_u32 v[2:3], s[14:15], v77, s70, v[78:79]
	v_and_b32_e32 v80, 0x70, v4
	v_mov_b32_e32 v81, v71
	v_lshl_add_u64 v[2:3], v[2:3], 0, v[80:81]
	s_lshl_b32 s2, s16, 1
	v_lshl_add_u64 v[2:3], v[2:3], 0, s[2:3]
	global_load_dwordx4 v[6:9], v[2:3], off offset:1024
	global_load_dwordx4 v[10:13], v[2:3], off offset:1152
	s_lshl_b32 s1, s76, 6
	s_and_b32 s1, s1, 0xc0
	v_lshrrev_b32_e32 v2, 2, v94
	v_and_or_b32 v2, v2, 48, s1
	v_lshl_add_u32 v4, v93, 6, s16
	v_or3_b32 v72, v2, v90, s0
	v_ashrrev_i32_e32 v5, 31, v4
	v_mad_u64_u32 v[2:3], s[14:15], v72, s70, v[78:79]
	v_lshlrev_b64 v[74:75], 1, v[4:5]
	v_lshl_add_u64 v[2:3], v[2:3], 0, v[74:75]
	v_or_b32_e32 v14, 64, v77
	v_lshl_add_u64 v[22:23], v[2:3], 0, v[70:71]
	v_mad_u64_u32 v[14:15], s[14:15], v14, s70, v[78:79]
	global_load_dwordx4 v[2:5], v[22:23], off
	v_lshl_add_u64 v[14:15], v[14:15], 0, v[80:81]
	v_lshl_add_u64 v[18:19], v[14:15], 0, s[2:3]
	s_mov_b32 s100, 0x60000
	s_mov_b32 s101, 0
	v_lshl_add_u64 v[248:249], v[18:19], 0, s[100:101]
	global_load_dwordx4 v[14:17], v[18:19], off offset:1024
	s_nop 0
	global_load_dwordx4 v[18:21], v[18:19], off offset:1152
	global_load_dword v250, v[248:249], off offset:1024
	global_load_dword v251, v[248:249], off offset:1152
	s_nop 0
	global_load_dwordx4 v[50:53], v[22:23], off offset:64
	v_mul_u32_u24_e32 v22, 0x90, v89
	v_add3_u32 v73, 0, v22, v80
	v_or_b32_e32 v22, 0x80, v77
	v_add3_u32 v91, v87, v70, v88
	s_mov_b32 s1, s3
	v_cmp_lt_i32_e32 vcc, v84, v85
	s_waitcnt vmcnt(7)
	ds_write_b128 v73, v[6:9]
	s_waitcnt vmcnt(6)
	ds_write_b128 v73, v[10:13] offset:9216
	v_mad_u64_u32 v[10:11], s[14:15], v22, s70, v[78:79]
	v_lshl_add_u64 v[10:11], v[10:11], 0, v[80:81]
	v_lshl_add_u64 v[26:27], v[10:11], 0, s[2:3]
	s_waitcnt lgkmcnt(0)
	s_barrier
	ds_read_b128 v[6:9], v91
	ds_read_b128 v[10:13], v91 offset:2304
	v_lshl_add_u64 v[248:249], v[26:27], 0, s[100:101]
	global_load_dwordx4 v[22:25], v[26:27], off offset:1024
	global_load_dwordx4 v[30:33], v[26:27], off offset:1152
	global_load_dword v250, v[248:249], off offset:1024
	global_load_dword v251, v[248:249], off offset:1152
	ds_read_b128 v[26:29], v91 offset:64
	ds_read_b128 v[34:37], v91 offset:4608
	ds_read_b128 v[38:41], v91 offset:2368
	ds_read_b128 v[42:45], v91 offset:4672
	ds_read_b128 v[46:49], v91 offset:6912
	s_waitcnt vmcnt(9) lgkmcnt(6)
	v_mfma_f32_16x16x32_bf16 v[6:9], v[6:9], v[2:5], 0
	ds_read_b128 v[54:57], v91 offset:6976
	s_waitcnt vmcnt(8)
	ds_write_b128 v73, v[14:17] offset:18432
	s_waitcnt vmcnt(7)
	ds_write_b128 v73, v[18:21] offset:27648
	s_waitcnt lgkmcnt(0)
	v_mfma_f32_16x16x32_bf16 v[10:13], v[10:13], v[2:5], 0
	s_barrier
	v_mfma_f32_16x16x32_bf16 v[14:17], v[34:37], v[2:5], 0
	v_mfma_f32_16x16x32_bf16 v[18:21], v[46:49], v[2:5], 0
	ds_read_b128 v[34:37], v91 offset:18432
	ds_read_b128 v[46:49], v91 offset:18496
	ds_read_b128 v[58:61], v91 offset:20736
	ds_read_b128 v[96:99], v91 offset:20800
	s_waitcnt vmcnt(4)
	v_mfma_f32_16x16x32_bf16 v[62:65], v[26:29], v[50:53], v[6:9]
	s_nop 2
	v_or_b32_e32 v6, s16, v89
	s_waitcnt lgkmcnt(1)
	v_mfma_f32_16x16x32_bf16 v[100:103], v[58:61], v[2:5], 0
	ds_read_b128 v[58:61], v91 offset:23040
	ds_read_b128 v[104:107], v91 offset:23104
	v_mul_u32_u24_e32 v8, 0x9000, v6
	v_mov_b32_e32 v7, v71
	v_mfma_f32_16x16x32_bf16 v[66:69], v[38:41], v[50:53], v[10:13]
	v_mov_b32_e32 v9, v71
	s_nop 1
	v_lshl_add_u64 v[10:11], s[4:5], 0, v[80:81]
	v_or_b32_e32 v12, 64, v6
	v_or_b32_e32 v13, 0xc0, v77
	v_lshl_add_u64 v[10:11], s[0:1], 1, v[10:11]
	v_lshlrev_b32_e32 v6, 1, v8
	v_mul_u32_u24_e32 v8, 0x9000, v12
	v_mad_u64_u32 v[12:13], s[0:1], v13, s70, v[78:79]
	v_lshl_add_u64 v[78:79], v[10:11], 0, v[6:7]
	v_lshlrev_b32_e32 v8, 1, v8
	v_lshl_add_u64 v[6:7], v[12:13], 0, v[80:81]
	v_lshl_add_u64 v[80:81], v[10:11], 0, v[8:9]
	v_lshl_add_u64 v[10:11], v[6:7], 0, s[2:3]
	s_waitcnt lgkmcnt(1)
	v_mfma_f32_16x16x32_bf16 v[108:111], v[58:61], v[2:5], 0
	ds_read_b128 v[58:61], v91 offset:25344
	ds_read_b128 v[112:115], v91 offset:25408
	global_load_dwordx4 v[6:9], v[10:11], off offset:1024
	s_nop 0
	global_load_dwordx4 v[10:13], v[10:11], off offset:1152
	v_mul_f32_e32 v38, 0x3e000000, v68
	s_waitcnt lgkmcnt(1)
	v_mfma_f32_16x16x32_bf16 v[116:119], v[58:61], v[2:5], 0
	v_mul_f32_e32 v39, 0x3e000000, v69
	s_waitcnt vmcnt(5)
	ds_write_b128 v73, v[22:25]
	s_waitcnt vmcnt(4)
	ds_write_b128 v73, v[30:33] offset:9216
	v_mfma_f32_16x16x32_bf16 v[58:61], v[42:45], v[50:53], v[14:17]
	s_waitcnt lgkmcnt(0)
	s_barrier
; #define LAS __attribute__((address_space(3)))
; template <bool LOCAL>
; __device__ __forceinline__ void na_unit(const bf16* P, const bf16* VT, bf16* YCAT, const LAS float* rpb_l, LAS bf16* buf, int b, int gr, int hp, int qblk, int tid) {
;     ...
;                 const int cc = c - NLOC;
; #pragma unroll
;                 for (int t4 = 0; t4 < 4; ++t4) {
;                     const LAS bf16* kp = cb + (16 * t4 + fr) * 72 + 8 * fq;
;                     f32x4 acc = {0.f, 0.f, 0.f, 0.f};
;                     acc = __builtin_amdgcn_mfma_f32_16x16x32_bf16(*(const LAS bf16x8*)(kp), qf[0], acc, 0, 0, 0);
;                     acc = __builtin_amdgcn_mfma_f32_16x16x32_bf16(*(const LAS bf16x8*)(kp + 32), qf[1], acc, 0, 0, 0);
; #pragma unroll
;                     for (int e = 0; e < 4; ++e) { acc[e] *= 0.125f; m = fmaxf(m, acc[e]); }
;                     sc[4 * (cc >= 0 ? cc : 0) + t4] = acc; }
;             }
;             if (sidx == NCH - 1) { m = fmaxf(m, __shfl_xor(m, 16)); m = fmaxf(m, __shfl_xor(m, 32)); }
	s_nop 0
	v_mul_f32_e32 v14, 0x3e000000, v62
	v_mul_f32_e32 v15, 0x3e000000, v63
	v_mfma_f32_16x16x32_bf16 v[54:57], v[54:57], v[50:53], v[18:21]
	s_nop 1
	v_mul_f32_e32 v40, 0x3e000000, v58
	v_mul_f32_e32 v41, 0x3e000000, v59
	v_mul_f32_e32 v77, 0x3e000000, v60
	v_mfma_f32_16x16x32_bf16 v[42:45], v[96:99], v[50:53], v[100:103]
	v_mul_f32_e32 v18, 0x3e000000, v64
	v_mul_f32_e32 v19, 0x3e000000, v65
	v_mul_f32_e32 v20, 0x3e000000, v66
	v_max3_f32 v100, v14, s73, v15
	v_mul_f32_e32 v21, 0x3e000000, v67
	v_max3_f32 v18, v100, v18, v19
	v_mfma_f32_16x16x32_bf16 v[34:37], v[34:37], v[2:5], 0
	v_max3_f32 v18, v18, v20, v21
	ds_read_b128 v[14:17], v91
	v_max3_f32 v22, v18, v38, v39
	ds_read_b128 v[18:21], v91 offset:2304
	v_mul_f32_e32 v95, 0x3e000000, v61
	v_max3_f32 v22, v22, v40, v41
	v_mul_f32_e32 v96, 0x3e000000, v54
	v_mul_f32_e32 v97, 0x3e000000, v55
	v_max3_f32 v38, v22, v77, v95
	v_mfma_f32_16x16x32_bf16 v[46:49], v[46:49], v[50:53], v[34:37]
	v_mul_f32_e32 v98, 0x3e000000, v56
	v_mul_f32_e32 v99, 0x3e000000, v57
	v_max3_f32 v38, v38, v96, v97
	ds_read_b128 v[22:25], v91 offset:64
	ds_read_b128 v[30:33], v91 offset:4608
	v_max3_f32 v38, v38, v98, v99
	ds_read_b128 v[96:99], v91 offset:2368
	v_mfma_f32_16x16x32_bf16 v[34:37], v[104:107], v[50:53], v[108:111]
	v_mul_f32_e32 v101, 0x3e000000, v46
	v_mul_f32_e32 v102, 0x3e000000, v47
	v_mul_f32_e32 v103, 0x3e000000, v48
	v_mul_f32_e32 v104, 0x3e000000, v49
	v_max3_f32 v38, v38, v101, v102
	v_mul_f32_e32 v108, 0x3e000000, v42
	v_mul_f32_e32 v109, 0x3e000000, v43
	s_waitcnt lgkmcnt(4)
	v_mfma_f32_16x16x32_bf16 v[14:17], v[14:17], v[2:5], 0
	v_max3_f32 v38, v38, v103, v104
	v_mul_f32_e32 v110, 0x3e000000, v44
	v_mul_f32_e32 v111, 0x3e000000, v45
	s_waitcnt lgkmcnt(3)
	v_mfma_f32_16x16x32_bf16 v[18:21], v[18:21], v[2:5], 0
	ds_read_b128 v[100:103], v91 offset:4672
	s_waitcnt lgkmcnt(2)
	v_mfma_f32_16x16x32_bf16 v[104:107], v[30:33], v[2:5], 0
	v_max3_f32 v30, v38, v108, v109
	v_max3_f32 v30, v30, v110, v111
	v_mfma_f32_16x16x32_bf16 v[26:29], v[112:115], v[50:53], v[116:119]
	v_mul_f32_e32 v112, 0x3e000000, v34
	v_mul_f32_e32 v113, 0x3e000000, v35
	v_mul_f32_e32 v114, 0x3e000000, v36
	v_mul_f32_e32 v115, 0x3e000000, v37
	v_max3_f32 v30, v30, v112, v113
	v_mfma_f32_16x16x32_bf16 v[38:41], v[22:25], v[50:53], v[14:17]
	s_nop 1
	v_mul_f32_e32 v116, 0x3e000000, v26
	v_mul_f32_e32 v117, 0x3e000000, v27
	v_mul_f32_e32 v118, 0x3e000000, v28
	v_max3_f32 v14, v30, v114, v115
	s_waitcnt lgkmcnt(1)
	v_mfma_f32_16x16x32_bf16 v[30:33], v[96:99], v[50:53], v[18:21]
	v_lshl_add_u64 v[248:249], v[78:79], 0, 0
	v_lshl_add_u64 v[238:239], v[80:81], 0, 0
	global_load_dwordx4 v[96:99], v[78:79], off
	global_load_dwordx4 v[108:111], v[80:81], off
	global_load_dword v250, v[248:249], off offset:128
	global_load_dword v251, v[238:239], off offset:128
	v_mul_f32_e32 v119, 0x3e000000, v29
	v_max3_f32 v14, v14, v116, v117
	v_max3_f32 v22, v14, v118, v119
	ds_read_b128 v[14:17], v91 offset:6912
	v_mul_f32_e32 v23, 0x3e000000, v38
	v_mul_f32_e32 v24, 0x3e000000, v39
	v_mul_f32_e32 v25, 0x3e000000, v40
	v_mul_f32_e32 v77, 0x3e000000, v41
	v_max3_f32 v22, v22, v23, v24
	s_waitcnt lgkmcnt(1)
	v_mfma_f32_16x16x32_bf16 v[18:21], v[100:103], v[50:53], v[104:107]
	v_mul_f32_e32 v95, 0x3e000000, v30
	v_mul_f32_e32 v100, 0x3e000000, v31
	v_max3_f32 v22, v22, v25, v77
	v_max3_f32 v77, v22, v95, v100
	ds_read_b128 v[22:25], v91 offset:6976
	s_waitcnt vmcnt(5)
	ds_write_b128 v73, v[6:9] offset:18432
	s_waitcnt vmcnt(4)
	ds_write_b128 v73, v[10:13] offset:27648
	s_waitcnt lgkmcnt(0)
	s_barrier
	ds_read_b128 v[6:9], v91 offset:18432
	v_mul_f32_e32 v101, 0x3e000000, v32
	v_mul_f32_e32 v10, 0x3e000000, v33
	v_mfma_f32_16x16x32_bf16 v[14:17], v[14:17], v[2:5], 0
	v_max3_f32 v77, v77, v101, v10
	ds_read_b128 v[10:13], v91 offset:18496
	v_mul_f32_e32 v95, 0x3e000000, v18
	v_mfma_f32_16x16x32_bf16 v[22:25], v[22:25], v[50:53], v[14:17]
	v_mul_f32_e32 v100, 0x3e000000, v21
	ds_read_b128 v[112:115], v91 offset:25408
	s_nop 1
	v_mul_f32_e32 v14, 0x3e000000, v19
	v_max3_f32 v77, v77, v95, v14
	s_waitcnt lgkmcnt(2)
	v_mfma_f32_16x16x32_bf16 v[6:9], v[6:9], v[2:5], 0
	ds_read_b128 v[14:17], v91 offset:20736
	v_mul_f32_e32 v95, 0x3e000000, v20
	v_max3_f32 v77, v77, v95, v100
	s_waitcnt lgkmcnt(2)
	v_mfma_f32_16x16x32_bf16 v[10:13], v[10:13], v[50:53], v[6:9]
	v_mul_f32_e32 v95, 0x3e000000, v22
	v_mul_f32_e32 v100, 0x3e000000, v23
	v_max3_f32 v77, v77, v95, v100
	ds_read_b128 v[6:9], v91 offset:20800
	s_waitcnt lgkmcnt(1)
	v_mfma_f32_16x16x32_bf16 v[14:17], v[14:17], v[2:5], 0
	ds_read_b128 v[100:103], v91 offset:23040
	v_mul_f32_e32 v95, 0x3e000000, v24
	v_mul_f32_e32 v104, 0x3e000000, v25
	s_waitcnt lgkmcnt(1)
	v_mfma_f32_16x16x32_bf16 v[14:17], v[6:9], v[50:53], v[14:17]
	ds_read_b128 v[6:9], v91 offset:23104
	v_max3_f32 v77, v77, v95, v104
	ds_read_b128 v[104:107], v91 offset:25344
	s_waitcnt lgkmcnt(2)
	v_mfma_f32_16x16x32_bf16 v[100:103], v[100:103], v[2:5], 0
	v_mul_f32_e32 v95, 0x3e000000, v10
	v_mul_f32_e32 v116, 0x3e000000, v11
	v_mul_f32_e32 v117, 0x3e000000, v12
	s_waitcnt lgkmcnt(1)
	v_mfma_f32_16x16x32_bf16 v[6:9], v[6:9], v[50:53], v[100:103]
	v_mul_f32_e32 v118, 0x3e000000, v13
	v_max3_f32 v77, v77, v95, v116
	v_mul_f32_e32 v119, 0x3e000000, v14
	v_mul_f32_e32 v120, 0x3e000000, v15
	s_waitcnt lgkmcnt(0)
	v_mfma_f32_16x16x32_bf16 v[2:5], v[104:107], v[2:5], 0
	v_max3_f32 v77, v77, v117, v118
	v_mul_f32_e32 v91, 0x3e000000, v16
	v_mul_f32_e32 v100, 0x3e000000, v17
	v_max3_f32 v77, v77, v119, v120
	v_mul_f32_e32 v101, 0x3e000000, v6
	v_mul_f32_e32 v102, 0x3e000000, v7
	v_max3_f32 v77, v77, v91, v100
	v_mul_f32_e32 v103, 0x3e000000, v8
	v_mul_f32_e32 v104, 0x3e000000, v9
	v_max3_f32 v77, v77, v101, v102
	v_mfma_f32_16x16x32_bf16 v[2:5], v[112:115], v[50:53], v[2:5]
	v_max3_f32 v77, v77, v103, v104
	v_lshl_add_u64 v[248:249], v[78:79], 0, 0
	v_lshl_add_u64 v[238:239], v[80:81], 0, 0
	global_load_dwordx4 v[100:103], v[78:79], off offset:128
	global_load_dwordx4 v[104:107], v[80:81], off offset:128
	global_load_dword v250, v[248:249], off offset:256
	global_load_dword v251, v[238:239], off offset:256
	s_waitcnt vmcnt(7)
	ds_write_b128 v73, v[96:99]
	s_waitcnt vmcnt(6)
	ds_write_b128 v73, v[108:111] offset:9216
	s_nop 0
	v_mul_f32_e32 v50, 0x3e000000, v2
	v_mul_f32_e32 v51, 0x3e000000, v3
	v_mul_f32_e32 v52, 0x3e000000, v4
	v_mul_f32_e32 v53, 0x3e000000, v5
	v_max3_f32 v50, v77, v50, v51
	v_max3_f32 v51, v50, v52, v53
	v_cndmask_b32_e32 v50, v83, v84, vcc
	v_lshlrev_b32_e32 v50, 2, v50
	ds_bpermute_b32 v52, v50, v51
	v_cmp_lt_i32_e32 vcc, v86, v85
	s_waitcnt lgkmcnt(0)
	s_barrier
; #define LAS __attribute__((address_space(3)))
; __device__ __forceinline__ unsigned cvt_pk_bf16(float lo, float hi) { const float __attribute__((ext_vector_type(2))) v = {lo, hi}; return __builtin_bit_cast(unsigned, __builtin_convertvector(v, bf16x2_t)); }
; template <bool LOCAL>
; __device__ __forceinline__ void na_unit(const bf16* P, const bf16* VT, bf16* YCAT, const LAS float* rpb_l, LAS bf16* buf, int b, int gr, int hp, int qblk, int tid) {
;     ...
;             if (sidx == NCH - 1) { m = fmaxf(m, __shfl_xor(m, 16)); m = fmaxf(m, __shfl_xor(m, 32)); }
;         } else {
;             const int c = sidx - NCH;
;             if (LOCAL && c < 8) {
;                 float p[8];
; #pragma unroll
;                 for (int e = 0; e < 4; ++e) { p[e] = __expf(sl[2 * (c < 8 ? c : 0)][e] - m); p[4 + e] = __expf(sl[2 * (c < 8 ? c : 0) + 1][e] - m); }
; #pragma unroll
;                 for (int e = 0; e < 8; ++e) lsum += p[e];
;                 const bf16x8 pf = __builtin_bit_cast(bf16x8, (v4u){pg8::cvt_pk_bf16(p[0], p[1]), pg8::cvt_pk_bf16(p[2], p[3]), pg8::cvt_pk_bf16(p[4], p[5]), pg8::cvt_pk_bf16(p[6], p[7])});
; #pragma unroll
;                 for (int dt = 0; dt < 4; ++dt) { const LAS bf16* vp = cb + (16 * dt + fr) * 72 + kc0 + 4 * fq;
;                     o[dt] = __builtin_amdgcn_mfma_f32_16x16x32_bf16(frag44(vp, vp + 16), pf, o[dt], 0, 0, 0); }
;             } else {
;                 const int cc = c - NLOC;
; #pragma unroll
;                 for (int p2 = 0; p2 < 2; ++p2) {
;                     float p[8];
; #pragma unroll
;                     for (int e = 0; e < 4; ++e) { p[e] = __expf(sc[4 * (cc >= 0 ? cc : 0) + 2 * p2][e] - m); p[4 + e] = __expf(sc[4 * (cc >= 0 ? cc : 0) + 2 * p2 + 1][e] - m); }
; #pragma unroll
;                     for (int e = 0; e < 8; ++e) lsum += p[e];
;                     const bf16x8 pf = __builtin_bit_cast(bf16x8, (v4u){pg8::cvt_pk_bf16(p[0], p[1]), pg8::cvt_pk_bf16(p[2], p[3]), pg8::cvt_pk_bf16(p[4], p[5]), pg8::cvt_pk_bf16(p[6], p[7])});
; #pragma unroll
;                     for (int dt = 0; dt < 4; ++dt) { const LAS bf16* vp = cb + (16 * dt + fr) * 72 + 32 * p2 + 4 * fq;
;                         o[dt] = __builtin_amdgcn_mfma_f32_16x16x32_bf16(frag44(vp, vp + 16), pf, o[dt], 0, 0, 0); }
	v_max_f32_e32 v52, v52, v52
	v_max_f32_e32 v52, v51, v52
	v_cndmask_b32_e32 v51, v83, v86, vcc
	v_lshlrev_b32_e32 v51, 2, v51
	ds_bpermute_b32 v53, v51, v52
	s_waitcnt lgkmcnt(0)
	v_max_f32_e32 v53, v53, v53
	v_max_f32_e32 v77, v52, v53
	v_fma_f32 v52, v62, s72, -v77
	v_fma_f32 v64, v64, s72, -v77
	v_mul_f32_e32 v52, 0x3fb8aa3b, v52
	v_fma_f32 v62, v63, s72, -v77
	v_mul_f32_e32 v64, 0x3fb8aa3b, v64
	v_fma_f32 v65, v65, s72, -v77
	v_exp_f32_e32 v53, v52
	v_fma_f32 v52, v66, s72, -v77
	v_mul_f32_e32 v62, 0x3fb8aa3b, v62
	v_exp_f32_e32 v66, v64
	v_fma_f32 v64, v68, s72, -v77
	v_mul_f32_e32 v65, 0x3fb8aa3b, v65
	v_add3_u32 v68, v87, v76, v88
	v_exp_f32_e32 v63, v62
	v_fma_f32 v62, v67, s72, -v77
	v_exp_f32_e32 v67, v65
	v_fma_f32 v65, v69, s72, -v77
	v_add_u32_e32 v69, 0x800, v68
	v_add_u32_e32 v91, 0x1000, v68
	v_add_u32_e32 v95, 0x1800, v68
	ds_read2_b64 v[96:99], v68 offset1:4
	ds_read2_b64 v[112:115], v69 offset0:32 offset1:36
	ds_read2_b64 v[116:119], v91 offset0:64 offset1:68
	ds_read2_b64 v[120:123], v95 offset0:96 offset1:100
	v_mul_f32_e32 v52, 0x3fb8aa3b, v52
	v_mul_f32_e32 v62, 0x3fb8aa3b, v62
	v_mul_f32_e32 v64, 0x3fb8aa3b, v64
	v_mul_f32_e32 v65, 0x3fb8aa3b, v65
	v_exp_f32_e32 v52, v52
	v_exp_f32_e32 v62, v62
	v_exp_f32_e32 v64, v64
	v_exp_f32_e32 v65, v65
	v_cvt_pk_bf16_f32 v108, v53, v63
	v_cvt_pk_bf16_f32 v109, v66, v67
	v_cvt_pk_bf16_f32 v110, v52, v62
	v_cvt_pk_bf16_f32 v111, v64, v65
	v_fma_f32 v58, v58, s72, -v77
	v_fma_f32 v54, v54, s72, -v77
	s_waitcnt lgkmcnt(3)
	v_mfma_f32_16x16x32_bf16 v[96:99], v[96:99], v[108:111], 0
	v_fma_f32 v59, v59, s72, -v77
	v_fma_f32 v55, v55, s72, -v77
	v_fma_f32 v60, v60, s72, -v77
	s_waitcnt lgkmcnt(2)
	v_mfma_f32_16x16x32_bf16 v[112:115], v[112:115], v[108:111], 0
	v_fma_f32 v56, v56, s72, -v77
	v_fma_f32 v61, v61, s72, -v77
	v_fma_f32 v57, v57, s72, -v77
	s_waitcnt lgkmcnt(1)
	v_mfma_f32_16x16x32_bf16 v[116:119], v[116:119], v[108:111], 0
	v_mul_f32_e32 v58, 0x3fb8aa3b, v58
	v_mul_f32_e32 v54, 0x3fb8aa3b, v54
	v_mul_f32_e32 v59, 0x3fb8aa3b, v59
	s_waitcnt lgkmcnt(0)
	v_mfma_f32_16x16x32_bf16 v[108:111], v[120:123], v[108:111], 0
	ds_read2_b64 v[120:123], v68 offset0:8 offset1:12
	v_mul_f32_e32 v55, 0x3fb8aa3b, v55
	v_mul_f32_e32 v60, 0x3fb8aa3b, v60
	v_mul_f32_e32 v56, 0x3fb8aa3b, v56
	v_mul_f32_e32 v61, 0x3fb8aa3b, v61
	v_mul_f32_e32 v57, 0x3fb8aa3b, v57
	v_exp_f32_e32 v58, v58
	v_exp_f32_e32 v54, v54
	v_exp_f32_e32 v59, v59
	v_exp_f32_e32 v55, v55
	v_exp_f32_e32 v60, v60
	v_exp_f32_e32 v56, v56
	v_exp_f32_e32 v61, v61
	v_exp_f32_e32 v57, v57
	v_cvt_pk_bf16_f32 v124, v58, v59
	v_cvt_pk_bf16_f32 v126, v54, v55
	v_cvt_pk_bf16_f32 v125, v60, v61
	v_cvt_pk_bf16_f32 v127, v56, v57
	v_fma_f32 v42, v42, s72, -v77
	v_mul_f32_e32 v42, 0x3fb8aa3b, v42
	s_waitcnt lgkmcnt(0)
	v_mfma_f32_16x16x32_bf16 v[96:99], v[120:123], v[124:127], v[96:99]
	ds_read2_b64 v[120:123], v69 offset0:40 offset1:44
	v_fma_f32 v46, v46, s72, -v77
	v_mul_f32_e32 v46, 0x3fb8aa3b, v46
	s_waitcnt lgkmcnt(0)
	v_mfma_f32_16x16x32_bf16 v[112:115], v[120:123], v[124:127], v[112:115]
	ds_read2_b64 v[120:123], v91 offset0:72 offset1:76
	v_add_u32_e32 v137, 0x5000, v68
	v_fma_f32 v26, v26, s72, -v77
	s_waitcnt lgkmcnt(0)
	v_mfma_f32_16x16x32_bf16 v[116:119], v[120:123], v[124:127], v[116:119]
	ds_read2_b64 v[120:123], v95 offset0:104 offset1:108
	v_lshl_add_u64 v[248:249], v[78:79], 0, 0
	v_lshl_add_u64 v[238:239], v[80:81], 0, 0
	global_load_dwordx4 v[128:131], v[78:79], off offset:256
	global_load_dwordx4 v[132:135], v[80:81], off offset:256
	global_load_dword v250, v[248:249], off offset:384
	global_load_dword v251, v[238:239], off offset:384
	s_waitcnt vmcnt(7)
	ds_write_b128 v73, v[100:103] offset:18432
	s_waitcnt vmcnt(6)
	ds_write_b128 v73, v[104:107] offset:27648
	s_waitcnt lgkmcnt(2)
	v_mfma_f32_16x16x32_bf16 v[108:111], v[120:123], v[124:127], v[108:111]
	v_exp_f32_e32 v121, v42
	v_fma_f32 v42, v47, s72, -v77
	v_mul_f32_e32 v42, 0x3fb8aa3b, v42
	v_exp_f32_e32 v122, v42
	v_fma_f32 v42, v43, s72, -v77
	v_mul_f32_e32 v42, 0x3fb8aa3b, v42
	v_exp_f32_e32 v123, v42
	v_fma_f32 v42, v48, s72, -v77
	v_mul_f32_e32 v42, 0x3fb8aa3b, v42
	v_exp_f32_e32 v124, v42
	v_fma_f32 v42, v44, s72, -v77
	v_mul_f32_e32 v42, 0x3fb8aa3b, v42
	v_add_u32_e32 v126, 0x4800, v68
	s_waitcnt lgkmcnt(0)
	s_barrier
; #define LAS __attribute__((address_space(3)))
; __device__ __forceinline__ unsigned cvt_pk_bf16(float lo, float hi) { const float __attribute__((ext_vector_type(2))) v = {lo, hi}; return __builtin_bit_cast(unsigned, __builtin_convertvector(v, bf16x2_t)); }
; template <bool LOCAL>
; __device__ __forceinline__ void na_unit(const bf16* P, const bf16* VT, bf16* YCAT, const LAS float* rpb_l, LAS bf16* buf, int b, int gr, int hp, int qblk, int tid) {
;     ...
;             } else {
;                 const int cc = c - NLOC;
; #pragma unroll
;                 for (int p2 = 0; p2 < 2; ++p2) {
;                     float p[8];
; #pragma unroll
;                     for (int e = 0; e < 4; ++e) { p[e] = __expf(sc[4 * (cc >= 0 ? cc : 0) + 2 * p2][e] - m); p[4 + e] = __expf(sc[4 * (cc >= 0 ? cc : 0) + 2 * p2 + 1][e] - m); }
; #pragma unroll
;                     for (int e = 0; e < 8; ++e) lsum += p[e];
;                     const bf16x8 pf = __builtin_bit_cast(bf16x8, (v4u){pg8::cvt_pk_bf16(p[0], p[1]), pg8::cvt_pk_bf16(p[2], p[3]), pg8::cvt_pk_bf16(p[4], p[5]), pg8::cvt_pk_bf16(p[6], p[7])});
; #pragma unroll
;                     for (int dt = 0; dt < 4; ++dt) { const LAS bf16* vp = cb + (16 * dt + fr) * 72 + 32 * p2 + 4 * fq;
;                         o[dt] = __builtin_amdgcn_mfma_f32_16x16x32_bf16(frag44(vp, vp + 16), pf, o[dt], 0, 0, 0); }
;                 }
	v_exp_f32_e32 v120, v46
	v_exp_f32_e32 v125, v42
	v_fma_f32 v42, v49, s72, -v77
	ds_read2_b64 v[46:49], v126 offset1:4
	v_mul_f32_e32 v42, 0x3fb8aa3b, v42
	v_exp_f32_e32 v127, v42
	v_fma_f32 v42, v45, s72, -v77
	v_mul_f32_e32 v42, 0x3fb8aa3b, v42
	v_exp_f32_e32 v136, v42
	v_cvt_pk_bf16_f32 v42, v120, v122
	v_cvt_pk_bf16_f32 v43, v124, v127
	v_cvt_pk_bf16_f32 v44, v121, v123
	v_cvt_pk_bf16_f32 v45, v125, v136
	v_mul_f32_e32 v26, 0x3fb8aa3b, v26
	v_fma_f32 v34, v34, s72, -v77
	s_waitcnt lgkmcnt(0)
	v_mfma_f32_16x16x32_bf16 v[46:49], v[46:49], v[42:45], v[96:99]
	v_mul_f32_e32 v34, 0x3fb8aa3b, v34
	v_fma_f32 v30, v30, s72, -v77
	v_mul_f32_e32 v30, 0x3fb8aa3b, v30
	ds_read2_b64 v[96:99], v137 offset0:32 offset1:36
	s_waitcnt lgkmcnt(0)
	v_mfma_f32_16x16x32_bf16 v[96:99], v[96:99], v[42:45], v[112:115]
	s_nop 2
	v_add_u32_e32 v112, 0x5800, v68
	v_add_u32_e32 v113, 0x6000, v68
	ds_read2_b64 v[100:103], v112 offset0:64 offset1:68
	ds_read2_b64 v[104:107], v113 offset0:96 offset1:100
	s_waitcnt lgkmcnt(1)
	v_mfma_f32_16x16x32_bf16 v[100:103], v[100:103], v[42:45], v[116:119]
	v_fma_f32 v38, v38, s72, -v77
	v_mul_f32_e32 v38, 0x3fb8aa3b, v38
	v_fma_f32 v18, v18, s72, -v77
	s_waitcnt lgkmcnt(0)
	v_mfma_f32_16x16x32_bf16 v[42:45], v[104:107], v[42:45], v[108:111]
	v_mul_f32_e32 v18, 0x3fb8aa3b, v18
	v_fma_f32 v10, v10, s72, -v77
	v_mul_f32_e32 v10, 0x3fb8aa3b, v10
	v_exp_f32_e32 v109, v26
	v_fma_f32 v26, v35, s72, -v77
	v_mul_f32_e32 v26, 0x3fb8aa3b, v26
	v_exp_f32_e32 v110, v26
	v_fma_f32 v26, v27, s72, -v77
	v_mul_f32_e32 v26, 0x3fb8aa3b, v26
	v_exp_f32_e32 v111, v26
	v_fma_f32 v26, v36, s72, -v77
	v_mul_f32_e32 v26, 0x3fb8aa3b, v26
	v_exp_f32_e32 v114, v26
	v_fma_f32 v26, v28, s72, -v77
	v_mul_f32_e32 v26, 0x3fb8aa3b, v26
	v_exp_f32_e32 v108, v34
	v_exp_f32_e32 v115, v26
	v_fma_f32 v26, v37, s72, -v77
	ds_read2_b64 v[34:37], v126 offset0:8 offset1:12
	v_mul_f32_e32 v26, 0x3fb8aa3b, v26
	v_exp_f32_e32 v116, v26
	v_fma_f32 v26, v29, s72, -v77
	v_mul_f32_e32 v26, 0x3fb8aa3b, v26
	v_exp_f32_e32 v117, v26
	v_cvt_pk_bf16_f32 v26, v108, v110
	v_cvt_pk_bf16_f32 v27, v114, v116
	v_cvt_pk_bf16_f32 v28, v109, v111
	v_cvt_pk_bf16_f32 v29, v115, v117
	v_fma_f32 v2, v2, s72, -v77
	v_mul_f32_e32 v2, 0x3fb8aa3b, v2
	s_waitcnt lgkmcnt(0)
	v_mfma_f32_16x16x32_bf16 v[34:37], v[34:37], v[26:29], v[46:49]
	v_fma_f32 v6, v6, s72, -v77
	v_mul_f32_e32 v6, 0x3fb8aa3b, v6
	s_nop 0
	ds_read2_b64 v[46:49], v137 offset0:40 offset1:44
	s_waitcnt lgkmcnt(0)
	v_mfma_f32_16x16x32_bf16 v[46:49], v[46:49], v[26:29], v[96:99]
	s_nop 2
	ds_read2_b64 v[96:99], v112 offset0:72 offset1:76
	s_waitcnt lgkmcnt(0)
	v_mfma_f32_16x16x32_bf16 v[96:99], v[96:99], v[26:29], v[100:103]
	s_nop 2
	ds_read2_b64 v[100:103], v113 offset0:104 offset1:108
	global_load_dwordx4 v[104:107], v[78:79], off offset:384
	s_nop 0
	global_load_dwordx4 v[78:81], v[80:81], off offset:384
	s_waitcnt vmcnt(5)
	ds_write_b128 v73, v[128:131]
	s_waitcnt vmcnt(4)
	ds_write_b128 v73, v[132:135] offset:9216
	s_waitcnt lgkmcnt(2)
	v_mfma_f32_16x16x32_bf16 v[26:29], v[100:103], v[26:29], v[42:45]
	v_exp_f32_e32 v101, v30
	v_fma_f32 v30, v39, s72, -v77
	v_mul_f32_e32 v30, 0x3fb8aa3b, v30
	v_exp_f32_e32 v102, v30
	v_fma_f32 v30, v31, s72, -v77
	v_mul_f32_e32 v30, 0x3fb8aa3b, v30
	v_exp_f32_e32 v103, v30
	v_fma_f32 v30, v40, s72, -v77
	v_mul_f32_e32 v30, 0x3fb8aa3b, v30
	v_exp_f32_e32 v118, v30
	v_fma_f32 v30, v32, s72, -v77
	v_mul_f32_e32 v30, 0x3fb8aa3b, v30
	s_waitcnt lgkmcnt(0)
	s_barrier
	v_exp_f32_e32 v100, v38
	v_exp_f32_e32 v119, v30
	v_fma_f32 v30, v41, s72, -v77
	ds_read2_b64 v[38:41], v68 offset1:4
	v_mul_f32_e32 v30, 0x3fb8aa3b, v30
	v_exp_f32_e32 v128, v30
	v_fma_f32 v30, v33, s72, -v77
	v_mul_f32_e32 v30, 0x3fb8aa3b, v30
	v_exp_f32_e32 v129, v30
	v_cvt_pk_bf16_f32 v30, v100, v102
	v_cvt_pk_bf16_f32 v31, v118, v128
	v_cvt_pk_bf16_f32 v32, v101, v103
	v_cvt_pk_bf16_f32 v33, v119, v129
	ds_read2_b64 v[42:45], v91 offset0:64 offset1:68
	s_waitcnt lgkmcnt(1)
	v_mfma_f32_16x16x32_bf16 v[34:37], v[38:41], v[30:33], v[34:37]
	ds_read2_b64 v[38:41], v69 offset0:32 offset1:36
	s_waitcnt lgkmcnt(0)
	v_mfma_f32_16x16x32_bf16 v[38:41], v[38:41], v[30:33], v[46:49]
	s_nop 2
	ds_read2_b64 v[46:49], v95 offset0:96 offset1:100
	s_waitcnt lgkmcnt(0)
	v_mfma_f32_16x16x32_bf16 v[26:29], v[46:49], v[30:33], v[26:29]
	v_exp_f32_e32 v46, v18
	v_fma_f32 v18, v22, s72, -v77
	v_mul_f32_e32 v18, 0x3fb8aa3b, v18
	v_exp_f32_e32 v47, v18
	v_fma_f32 v18, v19, s72, -v77
	v_mul_f32_e32 v18, 0x3fb8aa3b, v18
	v_exp_f32_e32 v48, v18
	v_fma_f32 v18, v23, s72, -v77
	v_mul_f32_e32 v18, 0x3fb8aa3b, v18
	v_exp_f32_e32 v49, v18
	v_fma_f32 v18, v20, s72, -v77
	v_mul_f32_e32 v18, 0x3fb8aa3b, v18
	v_mfma_f32_16x16x32_bf16 v[42:45], v[42:45], v[30:33], v[96:99]
	ds_read2_b64 v[30:33], v69 offset0:40 offset1:44
	s_nop 1
	v_exp_f32_e32 v96, v18
	v_fma_f32 v18, v24, s72, -v77
	v_mul_f32_e32 v18, 0x3fb8aa3b, v18
	v_exp_f32_e32 v97, v18
	v_fma_f32 v18, v21, s72, -v77
	v_mul_f32_e32 v22, 0x3fb8aa3b, v18
	ds_read2_b64 v[18:21], v68 offset0:8 offset1:12
	v_exp_f32_e32 v68, v22
	v_fma_f32 v22, v25, s72, -v77
	v_mul_f32_e32 v22, 0x3fb8aa3b, v22
	v_exp_f32_e32 v98, v22
	v_cvt_pk_bf16_f32 v22, v46, v48
	v_cvt_pk_bf16_f32 v23, v96, v68
	v_cvt_pk_bf16_f32 v24, v47, v49
	v_cvt_pk_bf16_f32 v25, v97, v98
	s_waitcnt lgkmcnt(0)
	s_nop 0
	v_mfma_f32_16x16x32_bf16 v[18:21], v[18:21], v[22:25], v[34:37]
	v_mfma_f32_16x16x32_bf16 v[30:33], v[30:33], v[22:25], v[38:41]
	s_nop 1
	ds_read2_b64 v[34:37], v91 offset0:72 offset1:76
	ds_read2_b64 v[38:41], v95 offset0:104 offset1:108
	s_waitcnt lgkmcnt(1)
	v_mfma_f32_16x16x32_bf16 v[34:37], v[34:37], v[22:25], v[42:45]
	s_waitcnt vmcnt(1)
	ds_write_b128 v73, v[104:107] offset:18432
	s_waitcnt vmcnt(0)
	ds_write_b128 v73, v[78:81] offset:27648
	s_waitcnt lgkmcnt(0)
	s_barrier
; #define LAS __attribute__((address_space(3)))
; __device__ __forceinline__ unsigned cvt_pk_bf16(float lo, float hi) { const float __attribute__((ext_vector_type(2))) v = {lo, hi}; return __builtin_bit_cast(unsigned, __builtin_convertvector(v, bf16x2_t)); }
; #define NA_STORE(sidx) do { LAS bf16* d_ = buf + ((sidx) & 1) * 9216; _Pragma("unroll") for (int q_ = 0; q_ < 2; ++q_) *(LAS v4u*)(d_ + q_ * 4608 + lrow * 72 + lseg * 8) = ld[(sidx) & 1][q_]; } while (0)
; template <bool LOCAL>
; __device__ __forceinline__ void na_unit(const bf16* P, const bf16* VT, bf16* YCAT, const LAS float* rpb_l, LAS bf16* buf, int b, int gr, int hp, int qblk, int tid) {
;     ...
;             } else {
;                 const int cc = c - NLOC;
; #pragma unroll
;                 for (int p2 = 0; p2 < 2; ++p2) {
;                     float p[8];
; #pragma unroll
;                     for (int e = 0; e < 4; ++e) { p[e] = __expf(sc[4 * (cc >= 0 ? cc : 0) + 2 * p2][e] - m); p[4 + e] = __expf(sc[4 * (cc >= 0 ? cc : 0) + 2 * p2 + 1][e] - m); }
; #pragma unroll
;                     for (int e = 0; e < 8; ++e) lsum += p[e];
;                     const bf16x8 pf = __builtin_bit_cast(bf16x8, (v4u){pg8::cvt_pk_bf16(p[0], p[1]), pg8::cvt_pk_bf16(p[2], p[3]), pg8::cvt_pk_bf16(p[4], p[5]), pg8::cvt_pk_bf16(p[6], p[7])});
; #pragma unroll
;                     for (int dt = 0; dt < 4; ++dt) { const LAS bf16* vp = cb + (16 * dt + fr) * 72 + 32 * p2 + 4 * fq;
;                         o[dt] = __builtin_amdgcn_mfma_f32_16x16x32_bf16(frag44(vp, vp + 16), pf, o[dt], 0, 0, 0); }
;                 }
;             }
;         }
;         if (sidx + 1 < 2 * NCH) NA_STORE(sidx + 1);
;         __syncthreads();
;     }
;     ...
;     lsum += __shfl_xor(lsum, 16); lsum += __shfl_xor(lsum, 32);
;     const float inv = 1.f / lsum;
;     bf16* op = YCAT + (size_t)(qrow0 + fr) * D + 512 + h * 64 + 4 * fq;
; #pragma unroll
;     for (int dt = 0; dt < 4; ++dt) { v2u w; w.x = pg8::cvt_pk_bf16(o[dt][0] * inv, o[dt][1] * inv); w.y = pg8::cvt_pk_bf16(o[dt][2] * inv, o[dt][3] * inv); *(v2u*)(op + dt * 16) = w; }
	v_mfma_f32_16x16x32_bf16 v[22:25], v[38:41], v[22:25], v[26:29]
	v_exp_f32_e32 v38, v10
	v_fma_f32 v10, v14, s72, -v77
	v_mul_f32_e32 v10, 0x3fb8aa3b, v10
	v_exp_f32_e32 v39, v10
	v_fma_f32 v10, v11, s72, -v77
	v_mul_f32_e32 v10, 0x3fb8aa3b, v10
	v_exp_f32_e32 v40, v10
	v_fma_f32 v10, v15, s72, -v77
	v_mul_f32_e32 v10, 0x3fb8aa3b, v10
	v_exp_f32_e32 v41, v10
	v_fma_f32 v10, v12, s72, -v77
	v_mul_f32_e32 v10, 0x3fb8aa3b, v10
	v_exp_f32_e32 v42, v10
	v_fma_f32 v10, v16, s72, -v77
	v_mul_f32_e32 v10, 0x3fb8aa3b, v10
	v_exp_f32_e32 v43, v10
	v_fma_f32 v10, v13, s72, -v77
	ds_read2_b64 v[26:29], v112 offset0:64 offset1:68
	v_mul_f32_e32 v14, 0x3fb8aa3b, v10
	v_exp_f32_e32 v44, v14
	v_fma_f32 v14, v17, s72, -v77
	v_mul_f32_e32 v14, 0x3fb8aa3b, v14
	v_exp_f32_e32 v45, v14
	v_cvt_pk_bf16_f32 v14, v38, v40
	v_cvt_pk_bf16_f32 v15, v42, v44
	v_cvt_pk_bf16_f32 v16, v39, v41
	v_cvt_pk_bf16_f32 v17, v43, v45
	ds_read2_b64 v[10:13], v126 offset1:4
	v_mov_b32_e32 v73, v71
	s_waitcnt lgkmcnt(1)
	v_mfma_f32_16x16x32_bf16 v[26:29], v[26:29], v[14:17], v[34:37]
	s_nop 2
	v_add_f32_e32 v34, 0, v53
	v_add_f32_e32 v34, v63, v34
	v_add_f32_e32 v34, v66, v34
	v_add_f32_e32 v34, v67, v34
	v_add_f32_e32 v34, v52, v34
	v_add_f32_e32 v34, v62, v34
	v_add_f32_e32 v34, v64, v34
	v_add_f32_e32 v34, v65, v34
	v_add_f32_e32 v34, v58, v34
	v_add_f32_e32 v34, v59, v34
	v_add_f32_e32 v34, v60, v34
	v_add_f32_e32 v34, v61, v34
	v_add_f32_e32 v34, v54, v34
	v_add_f32_e32 v34, v55, v34
	v_add_f32_e32 v34, v56, v34
	v_add_f32_e32 v34, v57, v34
	s_waitcnt lgkmcnt(0)
	v_mfma_f32_16x16x32_bf16 v[10:13], v[10:13], v[14:17], v[18:21]
	v_add_f32_e32 v34, v120, v34
	v_add_f32_e32 v34, v122, v34
	v_add_f32_e32 v34, v124, v34
	ds_read2_b64 v[18:21], v137 offset0:32 offset1:36
	v_add_f32_e32 v34, v127, v34
	v_add_f32_e32 v34, v121, v34
	v_add_f32_e32 v34, v123, v34
	v_add_f32_e32 v34, v125, v34
	v_add_f32_e32 v34, v136, v34
	v_add_f32_e32 v34, v108, v34
	s_waitcnt lgkmcnt(0)
	v_mfma_f32_16x16x32_bf16 v[18:21], v[18:21], v[14:17], v[30:33]
	v_add_f32_e32 v34, v110, v34
	s_nop 1
	ds_read2_b64 v[30:33], v113 offset0:96 offset1:100
	v_add_f32_e32 v34, v114, v34
	v_add_f32_e32 v34, v116, v34
	v_add_f32_e32 v34, v109, v34
	v_add_f32_e32 v34, v111, v34
	v_add_f32_e32 v34, v115, v34
	v_add_f32_e32 v34, v117, v34
	v_add_f32_e32 v34, v100, v34
	v_add_f32_e32 v34, v102, v34
	s_waitcnt lgkmcnt(0)
	v_mfma_f32_16x16x32_bf16 v[14:17], v[30:33], v[14:17], v[22:25]
	v_add_f32_e32 v34, v118, v34
	v_add_f32_e32 v34, v128, v34
	v_add_f32_e32 v34, v101, v34
	v_exp_f32_e32 v23, v2
	v_fma_f32 v2, v7, s72, -v77
	v_mul_f32_e32 v2, 0x3fb8aa3b, v2
	v_exp_f32_e32 v24, v2
	v_fma_f32 v2, v3, s72, -v77
	v_mul_f32_e32 v2, 0x3fb8aa3b, v2
	v_add_f32_e32 v34, v103, v34
	v_exp_f32_e32 v25, v2
	v_fma_f32 v2, v8, s72, -v77
	v_add_f32_e32 v34, v119, v34
	v_mul_f32_e32 v2, 0x3fb8aa3b, v2
	v_add_f32_e32 v34, v129, v34
	v_exp_f32_e32 v30, v2
	v_fma_f32 v2, v4, s72, -v77
	v_add_f32_e32 v34, v46, v34
	v_mul_f32_e32 v2, 0x3fb8aa3b, v2
	v_add_f32_e32 v34, v48, v34
	v_exp_f32_e32 v22, v6
	v_exp_f32_e32 v31, v2
	v_fma_f32 v2, v9, s72, -v77
	ds_read2_b64 v[6:9], v126 offset0:8 offset1:12
	v_add_f32_e32 v34, v96, v34
	v_mul_f32_e32 v2, 0x3fb8aa3b, v2
	v_add_f32_e32 v34, v68, v34
	v_exp_f32_e32 v32, v2
	v_fma_f32 v2, v5, s72, -v77
	v_add_f32_e32 v34, v47, v34
	v_mul_f32_e32 v2, 0x3fb8aa3b, v2
	v_add_f32_e32 v34, v49, v34
	v_exp_f32_e32 v33, v2
	v_add_f32_e32 v34, v97, v34
	v_add_f32_e32 v34, v98, v34
	v_add_f32_e32 v34, v38, v34
	v_add_f32_e32 v34, v40, v34
	v_cvt_pk_bf16_f32 v2, v22, v24
	v_cvt_pk_bf16_f32 v3, v30, v32
	v_cvt_pk_bf16_f32 v4, v23, v25
	v_cvt_pk_bf16_f32 v5, v31, v33
	v_add_f32_e32 v34, v42, v34
	v_add_f32_e32 v34, v44, v34
	s_waitcnt lgkmcnt(0)
	v_mfma_f32_16x16x32_bf16 v[6:9], v[6:9], v[2:5], v[10:13]
	v_add_f32_e32 v34, v39, v34
	v_add_f32_e32 v34, v41, v34
	v_add_f32_e32 v34, v43, v34
	ds_read2_b64 v[10:13], v137 offset0:40 offset1:44
	v_add_f32_e32 v34, v45, v34
	v_add_f32_e32 v22, v22, v34
	v_add_f32_e32 v22, v24, v22
	v_add_f32_e32 v22, v30, v22
	v_add_f32_e32 v22, v32, v22
	s_waitcnt lgkmcnt(0)
	v_mfma_f32_16x16x32_bf16 v[10:13], v[10:13], v[2:5], v[18:21]
	s_nop 2
	ds_read2_b64 v[18:21], v112 offset0:72 offset1:76
	v_add_f32_e32 v22, v23, v22
	v_add_f32_e32 v22, v25, v22
	v_add_f32_e32 v22, v31, v22
	v_add_f32_e32 v30, v33, v22
	ds_bpermute_b32 v31, v50, v30
	ds_read2_b64 v[22:25], v113 offset0:104 offset1:108
	s_waitcnt lgkmcnt(2)
	v_mfma_f32_16x16x32_bf16 v[18:21], v[18:21], v[2:5], v[26:29]
	v_mov_b32_e32 v77, v71
	s_waitcnt lgkmcnt(1)
	s_nop 0
	v_add_f32_e32 v26, v30, v31
	ds_bpermute_b32 v27, v51, v26
	s_waitcnt lgkmcnt(1)
	v_mfma_f32_16x16x32_bf16 v[14:17], v[22:25], v[2:5], v[14:17]
	s_waitcnt lgkmcnt(0)
	v_add_f32_e32 v2, v26, v27
	v_div_scale_f32 v3, s[0:1], v2, v2, 1.0
	v_rcp_f32_e32 v4, v3
	s_barrier
	s_mov_b64 s[0:1], 0
	v_fma_f32 v5, -v3, v4, 1.0
	v_fmac_f32_e32 v4, v5, v4
	v_div_scale_f32 v5, vcc, 1.0, v2, 1.0
	v_mul_f32_e32 v22, v5, v4
	v_fma_f32 v23, -v3, v22, v5
	v_fmac_f32_e32 v22, v23, v4
	v_fma_f32 v3, -v3, v22, v5
	v_div_fmas_f32 v3, v3, v4, v22
	v_div_fixup_f32 v22, v3, v2, 1.0
	v_lshlrev_b64 v[2:3], 11, v[72:73]
	v_lshl_add_u64 v[2:3], s[10:11], 0, v[2:3]
	v_lshl_add_u64 v[2:3], v[2:3], 0, v[74:75]
	v_pk_mul_f32 v[6:7], v[6:7], v[22:23] op_sel_hi:[1,0]
	v_pk_mul_f32 v[8:9], v[8:9], v[22:23] op_sel_hi:[1,0]
	v_lshl_add_u64 v[4:5], v[2:3], 0, v[76:77]
	v_cvt_pk_bf16_f32 v6, v6, v7
	v_cvt_pk_bf16_f32 v7, v8, v9
	global_store_dwordx2 v[4:5], v[6:7], off offset:1024
	v_pk_mul_f32 v[6:7], v[10:11], v[22:23] op_sel_hi:[1,0]
	v_pk_mul_f32 v[8:9], v[12:13], v[22:23] op_sel_hi:[1,0]
	v_cvt_pk_bf16_f32 v6, v6, v7
	v_cvt_pk_bf16_f32 v7, v8, v9
	global_store_dwordx2 v[4:5], v[6:7], off offset:1056
	v_pk_mul_f32 v[6:7], v[18:19], v[22:23] op_sel_hi:[1,0]
	v_pk_mul_f32 v[8:9], v[20:21], v[22:23] op_sel_hi:[1,0]
	v_cvt_pk_bf16_f32 v6, v6, v7
	v_cvt_pk_bf16_f32 v7, v8, v9
	v_lshl_add_u64 v[2:3], v[4:5], 0, s[12:13]
	global_store_dwordx2 v[4:5], v[6:7], off offset:1088
	v_pk_mul_f32 v[4:5], v[14:15], v[22:23] op_sel_hi:[1,0]
	v_pk_mul_f32 v[6:7], v[16:17], v[22:23] op_sel_hi:[1,0]
	v_cvt_pk_bf16_f32 v4, v4, v5

; #define LAS __attribute__((address_space(3)))
; template <bool LOCAL>
; __device__ __forceinline__ void na_unit(const bf16* P, const bf16* VT, bf16* YCAT, const LAS float* rpb_l, LAS bf16* buf, int b, int gr, int hp, int qblk, int tid) {
;     typedef pg8::bf16x8 bf16x8;
;     constexpr int NCH = LOCAL ? 12 : 4, NLOC = LOCAL ? 8 : 0;
;     const int lane = tid & 63, wv = tid >> 6, fr = lane & 15, fq = lane >> 4, hh = wv >> 2, qb = wv & 3, h = 2 * hp + hh;
;     const int qrow0 = LOCAL ? NCTX + b * SEQ + gr * 64 + 16 * qb : b * CTXL + qblk * 64 + 16 * qb;
;     const int r0 = min(max(gr - 4, 0), 24);
;     const int kc0 = qb == 0 ? 0 : qb == 1 ? 8 : qb == 2 ? 24 : 32;
;     const int qcol = 16 * qb + fr, cs = min(max(qcol - 8, 0), 48);
;     const LAS float* rpb = rpb_l + h * 15 * 31;
;     v4u ld[2][2];
;     const int lrow = (tid >> 3) & 63, lseg = tid & 7;
;     ...
;     bf16x8 qf[2];
; #pragma unroll
;     for (int ks = 0; ks < 2; ++ks) qf[ks] = *(const bf16x8*)(P + (size_t)(qrow0 + fr) * DINP + h * 64 + 32 * ks + 8 * fq);
;     f32x4 sl[16], sc[16];
;     float m = -1.0e30f, lsum = 0.f;
;     f32x4 o[4];
; #pragma unroll
;     for (int dt = 0; dt < 4; ++dt) o[dt] = (f32x4){0.f, 0.f, 0.f, 0.f};
;     NA_ISSUE(0); NA_ISSUE(1); NA_STORE(0);
;     __syncthreads();
; #pragma unroll
;     for (int sidx = 0; sidx < 2 * NCH; ++sidx) {
;         if (sidx + 2 < 2 * NCH) NA_ISSUE(sidx + 2);
;         const LAS bf16* cb = buf + (sidx & 1) * 9216 + hh * 4608;
;         if (sidx < NCH) {
;             const int c = sidx;
;             if (LOCAL && c < 8) {
; #pragma unroll
;                 for (int t2 = 0; t2 < 2; ++t2) {
;                     const LAS bf16* kp = cb + (kc0 + 16 * t2 + fr) * 72 + 8 * fq;
;                     f32x4 acc = {0.f, 0.f, 0.f, 0.f};
;                     acc = __builtin_amdgcn_mfma_f32_16x16x32_bf16(*(const LAS bf16x8*)(kp), qf[0], acc, 0, 0, 0);
;                     acc = __builtin_amdgcn_mfma_f32_16x16x32_bf16(*(const LAS bf16x8*)(kp + 32), qf[1], acc, 0, 0, 0);
;                     const LAS float* rb = rpb + (r0 + c - gr + 7) * 31 + 15 - qcol;
; #pragma unroll
;                     for (int e = 0; e < 4; ++e) { const int kcol = kc0 + 16 * t2 + 4 * fq + e; const bool ok = (kcol >= cs) && (kcol < cs + 16);
;                         const float sv = ok ? acc[e] * 0.125f + rb[ok ? kcol : qcol] : -1.0e30f; acc[e] = sv; m = fmaxf(m, sv); }
.LBB0_406:
	s_or_b64 exec, exec, s[0:1]
	s_bfe_u32 s19, s76, 0x50002
	v_sub_u32_e64 v3, s19, 4 clamp
	s_ashr_i32 s17, s76, 7
	v_readfirstlane_b32 s0, v3
	s_lshl_b32 s26, s17, 11
	s_min_u32 s20, s0, 24
	s_add_i32 s14, s26, 0x1000
	s_lshl_b32 s15, s20, 6
	s_or_b32 s16, s15, s14
	v_mov_b64_e32 v[18:19], s[8:9]
	v_and_b32_e32 v32, 7, v94
	v_or_b32_e32 v3, s16, v89
	s_and_b32 s18, s76, 3
	v_mad_i64_i32 v[4:5], s[0:1], v3, s70, v[18:19]
	v_lshlrev_b32_e32 v26, 4, v32
	v_mov_b32_e32 v27, v71
	v_lshl_add_u64 v[4:5], v[4:5], 0, v[26:27]
	s_lshl_b32 s2, s18, 8
	v_lshl_add_u64 v[4:5], v[4:5], 0, s[2:3]
	global_load_dwordx4 v[10:13], v[4:5], off offset:1024
	global_load_dwordx4 v[14:17], v[4:5], off offset:1152
	s_lshl_b32 s0, s19, 6
	v_lshl_or_b32 v31, v2, 4, v90
	v_lshl_add_u32 v33, s18, 1, v93
	s_or_b32 s0, s14, s0
	v_mad_u32_u24 v2, v89, s71, 0
	v_lshlrev_b32_e32 v72, 6, v33
	s_add_i32 s50, s26, 0x1040
	v_or_b32_e32 v74, s0, v31
	v_add_u32_e32 v75, v2, v26
	v_ashrrev_i32_e32 v73, 31, v72
	v_or_b32_e32 v4, s50, v89
	v_mad_i64_i32 v[2:3], s[0:1], v74, s70, v[18:19]
	v_add_u32_e32 v4, s15, v4
	v_lshl_add_u64 v[2:3], v[72:73], 1, v[2:3]
	v_mad_i64_i32 v[4:5], s[0:1], v4, s70, v[18:19]
	v_lshl_add_u64 v[2:3], v[2:3], 0, v[70:71]
	v_lshl_add_u64 v[20:21], v[4:5], 0, v[26:27]
	global_load_dwordx4 v[6:9], v[2:3], off
	s_nop 0
	global_load_dwordx4 v[2:5], v[2:3], off offset:64
	s_or_b32 s14, s26, s15
	s_addk_i32 s14, 0x1080
	v_or_b32_e32 v24, s14, v89
	v_mad_i64_i32 v[28:29], s[0:1], v24, s70, v[18:19]
	v_lshl_add_u64 v[26:27], v[28:29], 0, v[26:27]
	v_lshl_add_u64 v[22:23], v[20:21], 0, s[2:3]
	v_lshl_add_u64 v[26:27], v[26:27], 0, s[2:3]
	s_mov_b32 s100, 0x60000
	s_mov_b32 s101, 0
	v_lshl_add_u64 v[248:249], v[22:23], 0, s[100:101]
	global_load_dwordx4 v[18:21], v[22:23], off offset:1024
	s_nop 0
	global_load_dwordx4 v[22:25], v[22:23], off offset:1152
	global_load_dword v250, v[248:249], off offset:1024
	global_load_dword v251, v[248:249], off offset:1152
	v_add_u32_e32 v30, v87, v70
	v_add_u32_e32 v34, v91, v90
	v_mad_u32_u24 v36, v34, s71, v30
	s_movk_i32 s0, 0x744
	v_mul_lo_u32 v33, v33, s0
	s_sub_i32 s0, s20, s19
	s_mulk_i32 s0, 0x7c
	v_sub_u32_e64 v35, v31, 8 clamp
	s_add_i32 s0, s0, 0
	v_min_u32_e32 v35, 48, v35
	v_lshlrev_b32_e32 v77, 2, v92
	v_add_u32_e32 v33, s0, v33
	v_lshlrev_b32_e32 v31, 2, v31
	v_sub_u32_e32 v31, v33, v31
	v_add_u32_e32 v33, v91, v77
	v_cmp_ge_u32_e32 vcc, v33, v35
	v_mov_b32_e32 v92, 0xf149f2ca
	v_lshl_add_u32 v31, v33, 2, v31
	v_mov_b32_e32 v93, 0xf149f2ca
	s_waitcnt vmcnt(7)
	ds_write_b128 v75, v[10:13]
	s_waitcnt vmcnt(6)
	ds_write_b128 v75, v[14:17] offset:9216
	s_waitcnt lgkmcnt(0)
	s_barrier
	ds_read_b32 v240, v31 offset:37792
	ds_read_b32 v241, v31 offset:37796
	ds_read_b32 v242, v31 offset:37800
	ds_read_b32 v243, v31 offset:37804
	ds_read_b32 v244, v31 offset:37856
	ds_read_b32 v245, v31 offset:37860
	ds_read_b32 v246, v31 offset:37864
	ds_read_b32 v247, v31 offset:37868
	v_lshl_add_u64 v[248:249], v[26:27], 0, s[100:101]
	global_load_dwordx4 v[10:13], v[26:27], off offset:1024
	global_load_dwordx4 v[14:17], v[26:27], off offset:1152
	global_load_dword v250, v[248:249], off offset:1024
	global_load_dword v251, v[248:249], off offset:1152
	ds_read_b128 v[26:29], v36
	ds_read_b128 v[38:41], v36 offset:64
	s_waitcnt vmcnt(9) lgkmcnt(1)
	v_mfma_f32_16x16x32_bf16 v[26:29], v[26:29], v[6:9], 0
	v_add_u32_e32 v36, 16, v35
	v_cmp_lt_u32_e64 s[0:1], v33, v36
	s_and_b64 s[28:29], vcc, s[0:1]
	s_waitcnt vmcnt(8) lgkmcnt(0)
	v_mfma_f32_16x16x32_bf16 v[26:29], v[38:41], v[2:5], v[26:29]
	s_nop 2
	s_waitcnt lgkmcnt(0)
	s_nop 3
	v_fmac_f32_e32 v240, 0x3e000000, v26
	v_cndmask_b32_e64 v93, v93, v240, s[28:29]
	s_nop 4
	v_or_b32_e32 v26, 1, v33
	v_cmp_ge_u32_e32 vcc, v26, v35
	v_cmp_lt_u32_e64 s[0:1], v26, v36
	s_and_b64 s[30:31], vcc, s[0:1]
	s_nop 2
	s_waitcnt lgkmcnt(0)
	v_fmac_f32_e32 v241, 0x3e000000, v27
	v_cndmask_b32_e64 v92, v92, v241, s[30:31]
	v_or_b32_e32 v26, 2, v33
	v_cmp_ge_u32_e32 vcc, v26, v35
	v_cmp_lt_u32_e64 s[0:1], v26, v36
	s_and_b64 s[34:35], vcc, s[0:1]
	v_mov_b32_e32 v94, 0xf149f2ca
	v_mov_b32_e32 v95, 0xf149f2ca
	s_nop 2
	s_waitcnt lgkmcnt(0)
	v_fmac_f32_e32 v242, 0x3e000000, v28
	v_cndmask_b32_e64 v95, v95, v242, s[34:35]
	v_or_b32_e32 v26, 3, v33
	v_cmp_ge_u32_e32 vcc, v26, v35
	v_cmp_lt_u32_e64 s[0:1], v26, v36
	s_and_b64 s[36:37], vcc, s[0:1]
	s_nop 2
	s_waitcnt lgkmcnt(0)
	v_fmac_f32_e32 v243, 0x3e000000, v29
	v_cndmask_b32_e64 v94, v94, v243, s[36:37]
	v_add_u32_e32 v37, 16, v91
	v_add_u32_e32 v33, v37, v90
	v_mad_u32_u24 v38, v33, s71, v30
	ds_read_b128 v[26:29], v38
	ds_read_b128 v[38:41], v38 offset:64
	v_add_u32_e32 v37, v37, v77
	v_cmp_ge_u32_e32 vcc, v37, v35
	v_cmp_lt_u32_e64 s[0:1], v37, v36
	s_waitcnt lgkmcnt(1)
	v_mfma_f32_16x16x32_bf16 v[26:29], v[26:29], v[6:9], 0
	s_and_b64 s[38:39], vcc, s[0:1]
	v_mov_b32_e32 v96, 0xf149f2ca
	v_mov_b32_e32 v97, 0xf149f2ca
	s_waitcnt lgkmcnt(0)
	v_mfma_f32_16x16x32_bf16 v[26:29], v[38:41], v[2:5], v[26:29]
	s_nop 2
	s_waitcnt lgkmcnt(0)
	s_nop 3
	v_fmac_f32_e32 v244, 0x3e000000, v26
	v_cndmask_b32_e64 v97, v97, v244, s[38:39]
	s_nop 4
	v_or_b32_e32 v26, 1, v37
	v_cmp_ge_u32_e32 vcc, v26, v35
	v_cmp_lt_u32_e64 s[0:1], v26, v36
	s_and_b64 s[44:45], vcc, s[0:1]
	s_nop 2
	s_waitcnt lgkmcnt(0)
	v_fmac_f32_e32 v245, 0x3e000000, v27
	v_cndmask_b32_e64 v96, v96, v245, s[44:45]
	v_or_b32_e32 v26, 2, v37
	v_cmp_ge_u32_e32 vcc, v26, v35
	v_cmp_lt_u32_e64 s[0:1], v26, v36
	s_and_b64 s[46:47], vcc, s[0:1]
	v_mov_b32_e32 v98, 0xf149f2ca
	v_mov_b32_e32 v100, 0xf149f2ca
	s_nop 2
	s_waitcnt lgkmcnt(0)
	v_fmac_f32_e32 v246, 0x3e000000, v28
	v_cndmask_b32_e64 v100, v100, v246, s[46:47]
	v_or_b32_e32 v26, 3, v37
	v_cmp_ge_u32_e32 vcc, v26, v35
	v_cmp_lt_u32_e64 s[0:1], v26, v36
	s_and_b64 s[64:65], vcc, s[0:1]
	s_nop 2
	s_waitcnt lgkmcnt(0)
	v_fmac_f32_e32 v247, 0x3e000000, v29
	v_cndmask_b32_e64 v98, v98, v247, s[64:65]
	v_mul_u32_u24_e32 v27, 0x90, v34
	v_lshlrev_b32_e32 v26, 3, v32
	v_add_u32_e32 v32, v30, v27
	s_waitcnt vmcnt(7)
	ds_write_b128 v75, v[18:21] offset:18432
	s_waitcnt vmcnt(6)
	ds_write_b128 v75, v[22:25] offset:27648
	s_waitcnt lgkmcnt(0)
	s_barrier
; #define LAS __attribute__((address_space(3)))
; template <bool LOCAL>
; __device__ __forceinline__ void na_unit(const bf16* P, const bf16* VT, bf16* YCAT, const LAS float* rpb_l, LAS bf16* buf, int b, int gr, int hp, int qblk, int tid) {
;     ...
;         if (sidx < NCH) {
;             const int c = sidx;
;             if (LOCAL && c < 8) {
; #pragma unroll
;                 for (int t2 = 0; t2 < 2; ++t2) {
;                     const LAS bf16* kp = cb + (kc0 + 16 * t2 + fr) * 72 + 8 * fq;
;                     f32x4 acc = {0.f, 0.f, 0.f, 0.f};
;                     acc = __builtin_amdgcn_mfma_f32_16x16x32_bf16(*(const LAS bf16x8*)(kp), qf[0], acc, 0, 0, 0);
;                     acc = __builtin_amdgcn_mfma_f32_16x16x32_bf16(*(const LAS bf16x8*)(kp + 32), qf[1], acc, 0, 0, 0);
;                     const LAS float* rb = rpb + (r0 + c - gr + 7) * 31 + 15 - qcol;
; #pragma unroll
;                     for (int e = 0; e < 4; ++e) { const int kcol = kc0 + 16 * t2 + 4 * fq + e; const bool ok = (kcol >= cs) && (kcol < cs + 16);
;                         const float sv = ok ? acc[e] * 0.125f + rb[ok ? kcol : qcol] : -1.0e30f; acc[e] = sv; m = fmaxf(m, sv); }
;                     sl[2 * (c < 8 ? c : 0) + t2] = acc; }
	ds_read_b32 v240, v31 offset:37916
	ds_read_b32 v241, v31 offset:37920
	ds_read_b32 v242, v31 offset:37924
	ds_read_b32 v243, v31 offset:37928
	ds_read_b32 v244, v31 offset:37980
	ds_read_b32 v245, v31 offset:37984
	ds_read_b32 v246, v31 offset:37988
	ds_read_b32 v247, v31 offset:37992
	ds_read_b128 v[18:21], v32 offset:18432
	s_add_i32 s26, s26, s15
	s_add_i32 s0, s26, 0x10c0
	v_or_b32_e32 v24, s0, v89
	v_mov_b64_e32 v[22:23], s[8:9]
	s_lshl_b32 s1, s18, 7
	v_mad_i64_i32 v[22:23], s[18:19], v24, s70, v[22:23]
	v_lshlrev_b32_e32 v70, 1, v26
	v_lshl_add_u64 v[22:23], v[22:23], 0, v[70:71]
	s_lshl_b32 s2, s1, 1
	v_lshl_add_u64 v[22:23], v[22:23], 0, s[2:3]
	ds_read_b128 v[26:29], v32 offset:18496
	s_waitcnt lgkmcnt(1)
	v_mfma_f32_16x16x32_bf16 v[34:37], v[18:21], v[6:9], 0
	v_lshl_add_u64 v[248:249], v[22:23], 0, s[100:101]
	global_load_dwordx4 v[18:21], v[22:23], off offset:1024
	s_nop 0
	global_load_dwordx4 v[22:25], v[22:23], off offset:1152
	global_load_dword v250, v[248:249], off offset:1024
	global_load_dword v251, v[248:249], off offset:1152
	v_mov_b32_e32 v99, 0xf149f2ca
	v_mov_b32_e32 v101, 0xf149f2ca
	s_waitcnt lgkmcnt(0)
	v_mfma_f32_16x16x32_bf16 v[26:29], v[26:29], v[2:5], v[34:37]
	s_nop 2
	s_waitcnt lgkmcnt(0)
	s_nop 3
	v_fmac_f32_e32 v240, 0x3e000000, v26
	v_cndmask_b32_e64 v101, v101, v240, s[28:29]
	s_nop 2
	s_waitcnt lgkmcnt(0)
	s_nop 0
	v_fmac_f32_e32 v241, 0x3e000000, v27
	v_cndmask_b32_e64 v99, v99, v241, s[30:31]
	v_mov_b32_e32 v102, 0xf149f2ca
	v_mov_b32_e32 v103, 0xf149f2ca
	s_nop 2
	s_waitcnt lgkmcnt(0)
	v_fmac_f32_e32 v242, 0x3e000000, v28
	v_cndmask_b32_e64 v103, v103, v242, s[34:35]
	s_nop 2
	s_waitcnt lgkmcnt(0)
	v_fmac_f32_e32 v243, 0x3e000000, v29
	v_cndmask_b32_e64 v102, v102, v243, s[36:37]
	v_mul_u32_u24_e32 v26, 0x90, v33
	v_add_u32_e32 v33, v30, v26
	ds_read_b128 v[26:29], v33 offset:18432
	ds_read_b128 v[34:37], v33 offset:18496
	v_mov_b32_e32 v104, 0xf149f2ca
	v_mov_b32_e32 v106, 0xf149f2ca
	s_waitcnt lgkmcnt(1)
	v_mfma_f32_16x16x32_bf16 v[26:29], v[26:29], v[6:9], 0
	s_waitcnt lgkmcnt(0)
	v_mfma_f32_16x16x32_bf16 v[26:29], v[34:37], v[2:5], v[26:29]
	s_nop 2
	s_waitcnt lgkmcnt(0)
	s_nop 3
	v_fmac_f32_e32 v244, 0x3e000000, v26
	v_cndmask_b32_e64 v106, v106, v244, s[38:39]
	s_nop 2
	s_waitcnt lgkmcnt(0)
	s_nop 0
	v_fmac_f32_e32 v245, 0x3e000000, v27
	v_cndmask_b32_e64 v104, v104, v245, s[44:45]
	v_mov_b32_e32 v108, 0xf149f2ca
	v_mov_b32_e32 v110, 0xf149f2ca
	s_nop 2
	s_waitcnt lgkmcnt(0)
	v_fmac_f32_e32 v246, 0x3e000000, v28
	v_cndmask_b32_e64 v110, v110, v246, s[46:47]
	s_nop 2
	s_waitcnt lgkmcnt(0)
	v_fmac_f32_e32 v247, 0x3e000000, v29
	v_cndmask_b32_e64 v108, v108, v247, s[64:65]
	s_waitcnt vmcnt(7)
	ds_write_b128 v75, v[10:13]
	s_waitcnt vmcnt(6)
	ds_write_b128 v75, v[14:17] offset:9216
	s_waitcnt lgkmcnt(0)
	s_barrier
	ds_read_b32 v240, v31 offset:38040
	ds_read_b32 v241, v31 offset:38044
	ds_read_b32 v242, v31 offset:38048
	ds_read_b32 v243, v31 offset:38052
	ds_read_b32 v244, v31 offset:38104
	ds_read_b32 v245, v31 offset:38108
	ds_read_b32 v246, v31 offset:38112
	ds_read_b32 v247, v31 offset:38116
	ds_read_b128 v[10:13], v32
	ds_read_b128 v[26:29], v32 offset:64
	s_add_i32 s18, s26, 0x1100
	v_or_b32_e32 v16, s18, v89
	v_mov_b64_e32 v[14:15], s[8:9]
	v_mad_i64_i32 v[14:15], s[20:21], v16, s70, v[14:15]
	v_lshl_add_u64 v[14:15], v[14:15], 0, v[70:71]
	v_lshl_add_u64 v[14:15], v[14:15], 0, s[2:3]
	s_waitcnt lgkmcnt(1)
	v_mfma_f32_16x16x32_bf16 v[34:37], v[10:13], v[6:9], 0
	v_lshl_add_u64 v[248:249], v[14:15], 0, s[100:101]
	global_load_dwordx4 v[10:13], v[14:15], off offset:1024
	s_nop 0
	global_load_dwordx4 v[14:17], v[14:15], off offset:1152
	global_load_dword v250, v[248:249], off offset:1024
	global_load_dword v251, v[248:249], off offset:1152
	v_mov_b32_e32 v105, 0xf149f2ca
	v_mov_b32_e32 v107, 0xf149f2ca
	s_waitcnt lgkmcnt(0)
	v_mfma_f32_16x16x32_bf16 v[26:29], v[26:29], v[2:5], v[34:37]
	s_nop 2
	s_waitcnt lgkmcnt(0)
	s_nop 3
	v_fmac_f32_e32 v240, 0x3e000000, v26
	v_cndmask_b32_e64 v107, v107, v240, s[28:29]
	s_nop 2
	s_waitcnt lgkmcnt(0)
	s_nop 0
	v_fmac_f32_e32 v241, 0x3e000000, v27
	v_cndmask_b32_e64 v105, v105, v241, s[30:31]
	v_mov_b32_e32 v109, 0xf149f2ca
	v_mov_b32_e32 v111, 0xf149f2ca
	s_nop 2
	s_waitcnt lgkmcnt(0)
	v_fmac_f32_e32 v242, 0x3e000000, v28
	v_cndmask_b32_e64 v111, v111, v242, s[34:35]
	s_nop 2
	s_waitcnt lgkmcnt(0)
	v_fmac_f32_e32 v243, 0x3e000000, v29
	v_cndmask_b32_e64 v109, v109, v243, s[36:37]
	ds_read_b128 v[26:29], v33
	ds_read_b128 v[34:37], v33 offset:64
	v_mov_b32_e32 v112, 0xf149f2ca
	v_mov_b32_e32 v114, 0xf149f2ca
	s_waitcnt lgkmcnt(1)
	v_mfma_f32_16x16x32_bf16 v[26:29], v[26:29], v[6:9], 0
	s_waitcnt lgkmcnt(0)
	v_mfma_f32_16x16x32_bf16 v[26:29], v[34:37], v[2:5], v[26:29]
	s_nop 2
	s_waitcnt lgkmcnt(0)
	s_nop 3
	v_fmac_f32_e32 v244, 0x3e000000, v26
	v_cndmask_b32_e64 v114, v114, v244, s[38:39]
	s_nop 2
	s_waitcnt lgkmcnt(0)
	s_nop 0
	v_fmac_f32_e32 v245, 0x3e000000, v27
	v_cndmask_b32_e64 v112, v112, v245, s[44:45]
	v_mov_b32_e32 v113, 0xf149f2ca
	v_mov_b32_e32 v117, 0xf149f2ca
	s_nop 2
	s_waitcnt lgkmcnt(0)
	v_fmac_f32_e32 v246, 0x3e000000, v28
	v_cndmask_b32_e64 v117, v117, v246, s[46:47]
	s_nop 2
	s_waitcnt lgkmcnt(0)
	v_fmac_f32_e32 v247, 0x3e000000, v29
	v_cndmask_b32_e64 v113, v113, v247, s[64:65]
	s_waitcnt vmcnt(7)
	ds_write_b128 v75, v[18:21] offset:18432
	s_waitcnt vmcnt(6)
	ds_write_b128 v75, v[22:25] offset:27648
	s_waitcnt lgkmcnt(0)
	s_barrier
; #define LAS __attribute__((address_space(3)))
; template <bool LOCAL>
; __device__ __forceinline__ void na_unit(const bf16* P, const bf16* VT, bf16* YCAT, const LAS float* rpb_l, LAS bf16* buf, int b, int gr, int hp, int qblk, int tid) {
;     ...
;         if (sidx < NCH) {
;             const int c = sidx;
;             if (LOCAL && c < 8) {
; #pragma unroll
;                 for (int t2 = 0; t2 < 2; ++t2) {
;                     const LAS bf16* kp = cb + (kc0 + 16 * t2 + fr) * 72 + 8 * fq;
;                     f32x4 acc = {0.f, 0.f, 0.f, 0.f};
;                     acc = __builtin_amdgcn_mfma_f32_16x16x32_bf16(*(const LAS bf16x8*)(kp), qf[0], acc, 0, 0, 0);
;                     acc = __builtin_amdgcn_mfma_f32_16x16x32_bf16(*(const LAS bf16x8*)(kp + 32), qf[1], acc, 0, 0, 0);
;                     const LAS float* rb = rpb + (r0 + c - gr + 7) * 31 + 15 - qcol;
; #pragma unroll
;                     for (int e = 0; e < 4; ++e) { const int kcol = kc0 + 16 * t2 + 4 * fq + e; const bool ok = (kcol >= cs) && (kcol < cs + 16);
;                         const float sv = ok ? acc[e] * 0.125f + rb[ok ? kcol : qcol] : -1.0e30f; acc[e] = sv; m = fmaxf(m, sv); }
;                     sl[2 * (c < 8 ? c : 0) + t2] = acc; }
	ds_read_b32 v240, v31 offset:38164
	ds_read_b32 v241, v31 offset:38168
	ds_read_b32 v242, v31 offset:38172
	ds_read_b32 v243, v31 offset:38176
	ds_read_b32 v244, v31 offset:38228
	ds_read_b32 v245, v31 offset:38232
	ds_read_b32 v246, v31 offset:38236
	ds_read_b32 v247, v31 offset:38240
	ds_read_b128 v[18:21], v32 offset:18432
	ds_read_b128 v[26:29], v32 offset:18496
	s_add_i32 s20, s26, 0x1140
	v_or_b32_e32 v24, s20, v89
	v_mov_b64_e32 v[22:23], s[8:9]
	v_mad_i64_i32 v[22:23], s[22:23], v24, s70, v[22:23]
	v_lshl_add_u64 v[22:23], v[22:23], 0, v[70:71]
	v_lshl_add_u64 v[22:23], v[22:23], 0, s[2:3]
	s_waitcnt lgkmcnt(1)
	v_mfma_f32_16x16x32_bf16 v[34:37], v[18:21], v[6:9], 0
	v_lshl_add_u64 v[248:249], v[22:23], 0, s[100:101]
	global_load_dwordx4 v[18:21], v[22:23], off offset:1024
	s_nop 0
	global_load_dwordx4 v[22:25], v[22:23], off offset:1152
	global_load_dword v250, v[248:249], off offset:1024
	global_load_dword v251, v[248:249], off offset:1152
	v_mov_b32_e32 v115, 0xf149f2ca
	v_mov_b32_e32 v116, 0xf149f2ca
	s_waitcnt lgkmcnt(0)
	v_mfma_f32_16x16x32_bf16 v[26:29], v[26:29], v[2:5], v[34:37]
	s_nop 2
	s_waitcnt lgkmcnt(0)
	s_nop 3
	v_fmac_f32_e32 v240, 0x3e000000, v26
	v_cndmask_b32_e64 v116, v116, v240, s[28:29]
	s_nop 2
	s_waitcnt lgkmcnt(0)
	s_nop 0
	v_fmac_f32_e32 v241, 0x3e000000, v27
	v_cndmask_b32_e64 v115, v115, v241, s[30:31]
	v_mov_b32_e32 v118, 0xf149f2ca
	v_mov_b32_e32 v119, 0xf149f2ca
	s_nop 2
	s_waitcnt lgkmcnt(0)
	v_fmac_f32_e32 v242, 0x3e000000, v28
	v_cndmask_b32_e64 v119, v119, v242, s[34:35]
	s_nop 2
	s_waitcnt lgkmcnt(0)
	v_fmac_f32_e32 v243, 0x3e000000, v29
	v_cndmask_b32_e64 v118, v118, v243, s[36:37]
	ds_read_b128 v[26:29], v33 offset:18432
	ds_read_b128 v[34:37], v33 offset:18496
	v_mov_b32_e32 v120, 0xf149f2ca
	v_mov_b32_e32 v122, 0xf149f2ca
	s_waitcnt lgkmcnt(1)
	v_mfma_f32_16x16x32_bf16 v[26:29], v[26:29], v[6:9], 0
	s_waitcnt lgkmcnt(0)
	v_mfma_f32_16x16x32_bf16 v[26:29], v[34:37], v[2:5], v[26:29]
	s_nop 2
	s_waitcnt lgkmcnt(0)
	s_nop 3
	v_fmac_f32_e32 v244, 0x3e000000, v26
	v_cndmask_b32_e64 v122, v122, v244, s[38:39]
	s_nop 2
	s_waitcnt lgkmcnt(0)
	s_nop 0
	v_fmac_f32_e32 v245, 0x3e000000, v27
	v_cndmask_b32_e64 v120, v120, v245, s[44:45]
	v_mov_b32_e32 v121, 0xf149f2ca
	v_mov_b32_e32 v125, 0xf149f2ca
	s_nop 2
	s_waitcnt lgkmcnt(0)
	v_fmac_f32_e32 v246, 0x3e000000, v28
	v_cndmask_b32_e64 v125, v125, v246, s[46:47]
	s_nop 2
	s_waitcnt lgkmcnt(0)
	v_fmac_f32_e32 v247, 0x3e000000, v29
	v_cndmask_b32_e64 v121, v121, v247, s[64:65]
	s_waitcnt vmcnt(7)
	ds_write_b128 v75, v[10:13]
	s_waitcnt vmcnt(6)
	ds_write_b128 v75, v[14:17] offset:9216
	s_waitcnt lgkmcnt(0)
	s_barrier
	ds_read_b32 v240, v31 offset:38288
	ds_read_b32 v241, v31 offset:38292
	ds_read_b32 v242, v31 offset:38296
	ds_read_b32 v243, v31 offset:38300
	ds_read_b32 v244, v31 offset:38352
	ds_read_b32 v245, v31 offset:38356
	ds_read_b32 v246, v31 offset:38360
	ds_read_b32 v247, v31 offset:38364
	ds_read_b128 v[10:13], v32
	ds_read_b128 v[26:29], v32 offset:64
	s_add_i32 s22, s26, 0x1180
	v_or_b32_e32 v16, s22, v89
	v_mov_b64_e32 v[14:15], s[8:9]
	v_mad_i64_i32 v[14:15], s[24:25], v16, s70, v[14:15]
	v_lshl_add_u64 v[14:15], v[14:15], 0, v[70:71]
	v_lshl_add_u64 v[14:15], v[14:15], 0, s[2:3]
	s_waitcnt lgkmcnt(1)
	v_mfma_f32_16x16x32_bf16 v[34:37], v[10:13], v[6:9], 0
	v_lshl_add_u64 v[248:249], v[14:15], 0, s[100:101]
	global_load_dwordx4 v[10:13], v[14:15], off offset:1024
	s_nop 0
	global_load_dwordx4 v[14:17], v[14:15], off offset:1152
	global_load_dword v250, v[248:249], off offset:1024
	global_load_dword v251, v[248:249], off offset:1152
	v_mov_b32_e32 v123, 0xf149f2ca
	v_mov_b32_e32 v124, 0xf149f2ca
	s_waitcnt lgkmcnt(0)
	v_mfma_f32_16x16x32_bf16 v[26:29], v[26:29], v[2:5], v[34:37]
	s_nop 2
	s_waitcnt lgkmcnt(0)
	s_nop 3
	v_fmac_f32_e32 v240, 0x3e000000, v26
	v_cndmask_b32_e64 v124, v124, v240, s[28:29]
	s_nop 2
	s_waitcnt lgkmcnt(0)
	s_nop 0
	v_fmac_f32_e32 v241, 0x3e000000, v27
	v_cndmask_b32_e64 v123, v123, v241, s[30:31]
	v_mov_b32_e32 v126, 0xf149f2ca
	v_mov_b32_e32 v127, 0xf149f2ca
	s_nop 2
	s_waitcnt lgkmcnt(0)
	v_fmac_f32_e32 v242, 0x3e000000, v28
	v_cndmask_b32_e64 v127, v127, v242, s[34:35]
	s_nop 2
	s_waitcnt lgkmcnt(0)
	v_fmac_f32_e32 v243, 0x3e000000, v29
	v_cndmask_b32_e64 v126, v126, v243, s[36:37]
	ds_read_b128 v[26:29], v33
	ds_read_b128 v[34:37], v33 offset:64
	v_mov_b32_e32 v128, 0xf149f2ca
	v_mov_b32_e32 v130, 0xf149f2ca
	s_waitcnt lgkmcnt(1)
	v_mfma_f32_16x16x32_bf16 v[26:29], v[26:29], v[6:9], 0
	s_waitcnt lgkmcnt(0)
	v_mfma_f32_16x16x32_bf16 v[26:29], v[34:37], v[2:5], v[26:29]
	s_nop 2
	s_waitcnt lgkmcnt(0)
	s_nop 3
	v_fmac_f32_e32 v244, 0x3e000000, v26
	v_cndmask_b32_e64 v130, v130, v244, s[38:39]
	s_nop 2
	s_waitcnt lgkmcnt(0)
	s_nop 0
	v_fmac_f32_e32 v245, 0x3e000000, v27
	v_cndmask_b32_e64 v128, v128, v245, s[44:45]
	v_mov_b32_e32 v129, 0xf149f2ca
	v_mov_b32_e32 v134, 0xf149f2ca
	s_nop 2
	s_waitcnt lgkmcnt(0)
	v_fmac_f32_e32 v246, 0x3e000000, v28
	v_cndmask_b32_e64 v134, v134, v246, s[46:47]
	s_nop 2
	s_waitcnt lgkmcnt(0)
	v_fmac_f32_e32 v247, 0x3e000000, v29
	v_cndmask_b32_e64 v129, v129, v247, s[64:65]
	s_waitcnt vmcnt(7)
	ds_write_b128 v75, v[18:21] offset:18432
	s_waitcnt vmcnt(6)
	ds_write_b128 v75, v[22:25] offset:27648
	s_waitcnt lgkmcnt(0)
	s_barrier
; #define LAS __attribute__((address_space(3)))
; template <bool LOCAL>
; __device__ __forceinline__ void na_unit(const bf16* P, const bf16* VT, bf16* YCAT, const LAS float* rpb_l, LAS bf16* buf, int b, int gr, int hp, int qblk, int tid) {
;     ...
;         if (sidx < NCH) {
;             const int c = sidx;
;             if (LOCAL && c < 8) {
; #pragma unroll
;                 for (int t2 = 0; t2 < 2; ++t2) {
;                     const LAS bf16* kp = cb + (kc0 + 16 * t2 + fr) * 72 + 8 * fq;
;                     f32x4 acc = {0.f, 0.f, 0.f, 0.f};
;                     acc = __builtin_amdgcn_mfma_f32_16x16x32_bf16(*(const LAS bf16x8*)(kp), qf[0], acc, 0, 0, 0);
;                     acc = __builtin_amdgcn_mfma_f32_16x16x32_bf16(*(const LAS bf16x8*)(kp + 32), qf[1], acc, 0, 0, 0);
;                     const LAS float* rb = rpb + (r0 + c - gr + 7) * 31 + 15 - qcol;
; #pragma unroll
;                     for (int e = 0; e < 4; ++e) { const int kcol = kc0 + 16 * t2 + 4 * fq + e; const bool ok = (kcol >= cs) && (kcol < cs + 16);
;                         const float sv = ok ? acc[e] * 0.125f + rb[ok ? kcol : qcol] : -1.0e30f; acc[e] = sv; m = fmaxf(m, sv); }
;                     sl[2 * (c < 8 ? c : 0) + t2] = acc; }
;             } else {
;                 const int cc = c - NLOC;
; #pragma unroll
;                 for (int t4 = 0; t4 < 4; ++t4) {
;                     const LAS bf16* kp = cb + (16 * t4 + fr) * 72 + 8 * fq;
;                     f32x4 acc = {0.f, 0.f, 0.f, 0.f};
;                     acc = __builtin_amdgcn_mfma_f32_16x16x32_bf16(*(const LAS bf16x8*)(kp), qf[0], acc, 0, 0, 0);
;                     acc = __builtin_amdgcn_mfma_f32_16x16x32_bf16(*(const LAS bf16x8*)(kp + 32), qf[1], acc, 0, 0, 0);
; #pragma unroll
;                     for (int e = 0; e < 4; ++e) { acc[e] *= 0.125f; m = fmaxf(m, acc[e]); }
;                     sc[4 * (cc >= 0 ? cc : 0) + t4] = acc; }
	ds_read_b32 v240, v31 offset:38412
	ds_read_b32 v241, v31 offset:38416
	ds_read_b32 v242, v31 offset:38420
	ds_read_b32 v243, v31 offset:38424
	ds_read_b32 v244, v31 offset:38476
	ds_read_b32 v245, v31 offset:38480
	ds_read_b32 v246, v31 offset:38484
	ds_read_b32 v247, v31 offset:38488
	ds_read_b128 v[18:21], v32 offset:18432
	ds_read_b128 v[26:29], v32 offset:18496
	s_add_i32 s24, s26, 0x11c0
	v_or_b32_e32 v24, s24, v89
	v_mov_b64_e32 v[22:23], s[8:9]
	v_mad_i64_i32 v[22:23], s[26:27], v24, s70, v[22:23]
	v_lshl_add_u64 v[22:23], v[22:23], 0, v[70:71]
	v_lshl_add_u64 v[22:23], v[22:23], 0, s[2:3]
	s_waitcnt lgkmcnt(1)
	v_mfma_f32_16x16x32_bf16 v[34:37], v[18:21], v[6:9], 0
	global_load_dwordx4 v[18:21], v[22:23], off offset:1024
	s_nop 0
	global_load_dwordx4 v[22:25], v[22:23], off offset:1152
	v_mov_b32_e32 v131, 0xf149f2ca
	v_mov_b32_e32 v132, 0xf149f2ca
	s_waitcnt lgkmcnt(0)
	v_mfma_f32_16x16x32_bf16 v[26:29], v[26:29], v[2:5], v[34:37]
	s_nop 2
	s_waitcnt lgkmcnt(0)
	s_nop 3
	v_fmac_f32_e32 v240, 0x3e000000, v26
	v_cndmask_b32_e64 v132, v132, v240, s[28:29]
	s_nop 2
	s_waitcnt lgkmcnt(0)
	s_nop 0
	v_fmac_f32_e32 v241, 0x3e000000, v27
	v_cndmask_b32_e64 v131, v131, v241, s[30:31]
	v_mov_b32_e32 v135, 0xf149f2ca
	v_mov_b32_e32 v136, 0xf149f2ca
	s_nop 2
	s_waitcnt lgkmcnt(0)
	v_fmac_f32_e32 v242, 0x3e000000, v28
	v_cndmask_b32_e64 v136, v136, v242, s[34:35]
	s_nop 2
	s_waitcnt lgkmcnt(0)
	v_fmac_f32_e32 v243, 0x3e000000, v29
	v_cndmask_b32_e64 v135, v135, v243, s[36:37]
	ds_read_b128 v[26:29], v33 offset:18432
	ds_read_b128 v[34:37], v33 offset:18496
	v_mov_b32_e32 v138, 0xf149f2ca
	v_mov_b32_e32 v140, 0xf149f2ca
	s_waitcnt lgkmcnt(1)
	v_mfma_f32_16x16x32_bf16 v[26:29], v[26:29], v[6:9], 0
	s_waitcnt lgkmcnt(0)
	v_mfma_f32_16x16x32_bf16 v[26:29], v[34:37], v[2:5], v[26:29]
	s_nop 2
	s_waitcnt lgkmcnt(0)
	s_nop 3
	v_fmac_f32_e32 v244, 0x3e000000, v26
	v_cndmask_b32_e64 v140, v140, v244, s[38:39]
	s_nop 2
	s_waitcnt lgkmcnt(0)
	s_nop 0
	v_fmac_f32_e32 v245, 0x3e000000, v27
	v_cndmask_b32_e64 v138, v138, v245, s[44:45]
	v_mov_b32_e32 v139, 0xf149f2ca
	v_mov_b32_e32 v143, 0xf149f2ca
	s_nop 2
	s_waitcnt lgkmcnt(0)
	v_fmac_f32_e32 v246, 0x3e000000, v28
	v_cndmask_b32_e64 v143, v143, v246, s[46:47]
	s_nop 2
	s_waitcnt lgkmcnt(0)
	v_fmac_f32_e32 v247, 0x3e000000, v29
	v_cndmask_b32_e64 v139, v139, v247, s[64:65]
	s_waitcnt vmcnt(5)
	ds_write_b128 v75, v[10:13]
	s_waitcnt vmcnt(4)
	ds_write_b128 v75, v[14:17] offset:9216
	s_waitcnt lgkmcnt(0)
	s_barrier
	ds_read_b32 v240, v31 offset:38536
	ds_read_b32 v241, v31 offset:38540
	ds_read_b32 v242, v31 offset:38544
	ds_read_b32 v243, v31 offset:38548
	ds_read_b32 v244, v31 offset:38600
	ds_read_b32 v245, v31 offset:38604
	ds_read_b32 v246, v31 offset:38608
	ds_read_b32 v247, v31 offset:38612
	ds_read_b128 v[10:13], v32
	ds_read_b128 v[26:29], v32 offset:64
	s_lshl_b32 s26, s17, 8
	v_or_b32_e32 v34, s26, v89
	v_mov_b64_e32 v[14:15], s[8:9]
	v_mad_i64_i32 v[14:15], s[52:53], v34, s70, v[14:15]
	v_lshl_add_u64 v[14:15], v[14:15], 0, v[70:71]
	v_lshl_add_u64 v[14:15], v[14:15], 0, s[2:3]
	s_waitcnt lgkmcnt(1)
	v_mfma_f32_16x16x32_bf16 v[36:39], v[10:13], v[6:9], 0
	v_lshl_add_u64 v[248:249], v[14:15], 0, s[100:101]
	global_load_dwordx4 v[10:13], v[14:15], off offset:1024
	s_nop 0
	global_load_dwordx4 v[14:17], v[14:15], off offset:1152
	global_load_dword v250, v[248:249], off offset:1024
	global_load_dword v251, v[248:249], off offset:1152
	v_mov_b32_e32 v141, 0xf149f2ca
	v_mov_b32_e32 v142, 0xf149f2ca
	s_waitcnt lgkmcnt(0)
	v_mfma_f32_16x16x32_bf16 v[26:29], v[26:29], v[2:5], v[36:39]
	s_nop 2
	s_waitcnt lgkmcnt(0)
	s_nop 3
	v_fmac_f32_e32 v240, 0x3e000000, v26
	v_cndmask_b32_e64 v142, v142, v240, s[28:29]
	s_nop 2
	s_waitcnt lgkmcnt(0)
	s_nop 0
	v_fmac_f32_e32 v241, 0x3e000000, v27
	v_cndmask_b32_e64 v141, v141, v241, s[30:31]
	v_mov_b32_e32 v144, 0xf149f2ca
	v_mov_b32_e32 v145, 0xf149f2ca
	s_nop 2
	s_waitcnt lgkmcnt(0)
	v_fmac_f32_e32 v242, 0x3e000000, v28
	v_cndmask_b32_e64 v145, v145, v242, s[34:35]
	s_nop 2
	s_waitcnt lgkmcnt(0)
	v_fmac_f32_e32 v243, 0x3e000000, v29
	v_cndmask_b32_e64 v144, v144, v243, s[36:37]
	ds_read_b128 v[26:29], v33
	ds_read_b128 v[36:39], v33 offset:64
	v_mov_b32_e32 v148, 0xf149f2ca
	v_mov_b32_e32 v150, 0xf149f2ca
	s_waitcnt lgkmcnt(1)
	v_mfma_f32_16x16x32_bf16 v[26:29], v[26:29], v[6:9], 0
	s_waitcnt lgkmcnt(0)
	v_mfma_f32_16x16x32_bf16 v[26:29], v[36:39], v[2:5], v[26:29]
	s_nop 2
	s_waitcnt lgkmcnt(0)
	s_nop 3
	v_fmac_f32_e32 v244, 0x3e000000, v26
	v_cndmask_b32_e64 v150, v150, v244, s[38:39]
	s_nop 2
	s_waitcnt lgkmcnt(0)
	s_nop 0
	v_fmac_f32_e32 v245, 0x3e000000, v27
	v_cndmask_b32_e64 v148, v148, v245, s[44:45]
	v_mov_b32_e32 v149, 0xf149f2ca
	v_mov_b32_e32 v153, 0xf149f2ca
	s_nop 2
	s_waitcnt lgkmcnt(0)
	v_fmac_f32_e32 v246, 0x3e000000, v28
	v_cndmask_b32_e64 v153, v153, v246, s[46:47]
	s_nop 2
	s_waitcnt lgkmcnt(0)
	v_fmac_f32_e32 v247, 0x3e000000, v29
	v_cndmask_b32_e64 v149, v149, v247, s[64:65]
	s_waitcnt vmcnt(5)
	ds_write_b128 v75, v[18:21] offset:18432
	s_waitcnt vmcnt(4)
	ds_write_b128 v75, v[22:25] offset:27648
	s_waitcnt lgkmcnt(0)
	s_barrier
; #define LAS __attribute__((address_space(3)))
; template <bool LOCAL>
; __device__ __forceinline__ void na_unit(const bf16* P, const bf16* VT, bf16* YCAT, const LAS float* rpb_l, LAS bf16* buf, int b, int gr, int hp, int qblk, int tid) {
;     ...
;         if (sidx < NCH) {
;             const int c = sidx;
;             if (LOCAL && c < 8) {
; #pragma unroll
;                 for (int t2 = 0; t2 < 2; ++t2) {
;                     const LAS bf16* kp = cb + (kc0 + 16 * t2 + fr) * 72 + 8 * fq;
;                     f32x4 acc = {0.f, 0.f, 0.f, 0.f};
;                     acc = __builtin_amdgcn_mfma_f32_16x16x32_bf16(*(const LAS bf16x8*)(kp), qf[0], acc, 0, 0, 0);
;                     acc = __builtin_amdgcn_mfma_f32_16x16x32_bf16(*(const LAS bf16x8*)(kp + 32), qf[1], acc, 0, 0, 0);
;                     const LAS float* rb = rpb + (r0 + c - gr + 7) * 31 + 15 - qcol;
; #pragma unroll
;                     for (int e = 0; e < 4; ++e) { const int kcol = kc0 + 16 * t2 + 4 * fq + e; const bool ok = (kcol >= cs) && (kcol < cs + 16);
;                         const float sv = ok ? acc[e] * 0.125f + rb[ok ? kcol : qcol] : -1.0e30f; acc[e] = sv; m = fmaxf(m, sv); }
;                     sl[2 * (c < 8 ? c : 0) + t2] = acc; }
;             } else {
;                 const int cc = c - NLOC;
; #pragma unroll
;                 for (int t4 = 0; t4 < 4; ++t4) {
;                     const LAS bf16* kp = cb + (16 * t4 + fr) * 72 + 8 * fq;
;                     f32x4 acc = {0.f, 0.f, 0.f, 0.f};
;                     acc = __builtin_amdgcn_mfma_f32_16x16x32_bf16(*(const LAS bf16x8*)(kp), qf[0], acc, 0, 0, 0);
;                     acc = __builtin_amdgcn_mfma_f32_16x16x32_bf16(*(const LAS bf16x8*)(kp + 32), qf[1], acc, 0, 0, 0);
; #pragma unroll
;                     for (int e = 0; e < 4; ++e) { acc[e] *= 0.125f; m = fmaxf(m, acc[e]); }
;                     sc[4 * (cc >= 0 ? cc : 0) + t4] = acc; }
;             }
;             if (sidx == NCH - 1) { m = fmaxf(m, __shfl_xor(m, 16)); m = fmaxf(m, __shfl_xor(m, 32)); }
	ds_read_b32 v240, v31 offset:38660
	ds_read_b32 v241, v31 offset:38664
	ds_read_b32 v242, v31 offset:38668
	ds_read_b32 v243, v31 offset:38672
	ds_read_b32 v244, v31 offset:38724
	ds_read_b32 v245, v31 offset:38728
	ds_read_b32 v246, v31 offset:38732
	ds_read_b32 v247, v31 offset:38736
	ds_read_b128 v[18:21], v32 offset:18432
	ds_read_b128 v[26:29], v32 offset:18496
	v_or_b32_e32 v24, 64, v34
	v_mov_b64_e32 v[22:23], s[8:9]
	v_mad_i64_i32 v[22:23], s[52:53], v24, s70, v[22:23]
	v_lshl_add_u64 v[22:23], v[22:23], 0, v[70:71]
	v_lshl_add_u64 v[22:23], v[22:23], 0, s[2:3]
	s_waitcnt lgkmcnt(1)
	v_mfma_f32_16x16x32_bf16 v[36:39], v[18:21], v[6:9], 0
	v_lshl_add_u64 v[248:249], v[22:23], 0, s[100:101]
	global_load_dwordx4 v[18:21], v[22:23], off offset:1024
	s_nop 0
	global_load_dwordx4 v[22:25], v[22:23], off offset:1152
	global_load_dword v250, v[248:249], off offset:1024
	global_load_dword v251, v[248:249], off offset:1152
	v_mov_b32_e32 v151, 0xf149f2ca
	v_mov_b32_e32 v152, 0xf149f2ca
	s_waitcnt lgkmcnt(0)
	v_mfma_f32_16x16x32_bf16 v[26:29], v[26:29], v[2:5], v[36:39]
	s_nop 2
	s_waitcnt lgkmcnt(0)
	s_nop 3
	v_fmac_f32_e32 v240, 0x3e000000, v26
	v_cndmask_b32_e64 v152, v152, v240, s[28:29]
	s_nop 2
	s_waitcnt lgkmcnt(0)
	s_nop 0
	v_fmac_f32_e32 v241, 0x3e000000, v27
	v_cndmask_b32_e64 v151, v151, v241, s[30:31]
	v_mov_b32_e32 v154, 0xf149f2ca
	v_mov_b32_e32 v155, 0xf149f2ca
	s_nop 2
	s_waitcnt lgkmcnt(0)
	v_fmac_f32_e32 v242, 0x3e000000, v28
	v_cndmask_b32_e64 v155, v155, v242, s[34:35]
	s_nop 2
	s_waitcnt lgkmcnt(0)
	v_fmac_f32_e32 v243, 0x3e000000, v29
	v_cndmask_b32_e64 v154, v154, v243, s[36:37]
	ds_read_b128 v[26:29], v33 offset:18432
	ds_read_b128 v[36:39], v33 offset:18496
	v_mov_b32_e32 v156, 0xf149f2ca
	v_mov_b32_e32 v158, 0xf149f2ca
	s_waitcnt lgkmcnt(1)
	v_mfma_f32_16x16x32_bf16 v[26:29], v[26:29], v[6:9], 0
	s_waitcnt lgkmcnt(0)
	v_mfma_f32_16x16x32_bf16 v[26:29], v[36:39], v[2:5], v[26:29]
	s_nop 2
	s_waitcnt lgkmcnt(0)
	s_nop 3
	v_fmac_f32_e32 v244, 0x3e000000, v26
	v_cndmask_b32_e64 v158, v158, v244, s[38:39]
	s_nop 2
	s_waitcnt lgkmcnt(0)
	s_nop 0
	v_fmac_f32_e32 v245, 0x3e000000, v27
	v_cndmask_b32_e64 v156, v156, v245, s[44:45]
	v_mov_b32_e32 v157, 0xf149f2ca
	v_mov_b32_e32 v160, 0xf149f2ca
	s_nop 2
	s_waitcnt lgkmcnt(0)
	v_fmac_f32_e32 v246, 0x3e000000, v28
	v_cndmask_b32_e64 v160, v160, v246, s[46:47]
	s_nop 2
	s_waitcnt lgkmcnt(0)
	v_fmac_f32_e32 v247, 0x3e000000, v29
	v_cndmask_b32_e64 v157, v157, v247, s[64:65]
	v_max3_f32 v26, v93, s73, v92
	v_max3_f32 v26, v26, v95, v94
	v_max3_f32 v26, v26, v97, v96
	v_max3_f32 v26, v26, v100, v98
	v_max3_f32 v26, v26, v101, v99
	v_max3_f32 v26, v26, v103, v102
	v_max3_f32 v26, v26, v106, v104
	v_max3_f32 v26, v26, v110, v108
	v_max3_f32 v26, v26, v107, v105
	v_max3_f32 v26, v26, v111, v109
	v_max3_f32 v26, v26, v114, v112
	v_max3_f32 v26, v26, v117, v113
	v_max3_f32 v26, v26, v116, v115
	v_max3_f32 v26, v26, v119, v118
	v_max3_f32 v26, v26, v122, v120
	v_max3_f32 v26, v26, v125, v121
	v_max3_f32 v26, v26, v124, v123
	v_max3_f32 v26, v26, v127, v126
	v_max3_f32 v26, v26, v130, v128
	v_max3_f32 v26, v26, v134, v129
	v_max3_f32 v26, v26, v132, v131
	v_max3_f32 v26, v26, v136, v135
	v_max3_f32 v26, v26, v140, v138
	v_max3_f32 v26, v26, v143, v139
	v_max3_f32 v26, v26, v142, v141
	v_max3_f32 v26, v26, v145, v144
	v_mad_u32_u24 v90, v90, s71, v30
	v_max3_f32 v26, v26, v150, v148
	s_waitcnt vmcnt(7)
	ds_write_b128 v75, v[10:13]
	s_waitcnt vmcnt(6)
	ds_write_b128 v75, v[14:17] offset:9216
	s_waitcnt lgkmcnt(0)
	s_barrier
	ds_read_b128 v[10:13], v90
	ds_read_b128 v[14:17], v90 offset:64
	v_max3_f32 v26, v26, v153, v149
	v_max3_f32 v26, v26, v152, v151
	v_max3_f32 v26, v26, v155, v154
	v_max3_f32 v26, v26, v158, v156
	v_max3_f32 v35, v26, v160, v157
	v_or_b32_e32 v26, 0x80, v34
	v_mov_b64_e32 v[44:45], s[8:9]
	v_mad_i64_i32 v[26:27], s[28:29], v26, s70, v[44:45]
	v_lshl_add_u64 v[26:27], v[26:27], 0, v[70:71]
	v_lshl_add_u64 v[30:31], v[26:27], 0, s[2:3]
	s_waitcnt lgkmcnt(1)
	v_mfma_f32_16x16x32_bf16 v[10:13], v[10:13], v[6:9], 0
	v_lshl_add_u64 v[248:249], v[30:31], 0, s[100:101]
	global_load_dwordx4 v[26:29], v[30:31], off offset:1024
	s_nop 0
	global_load_dwordx4 v[30:33], v[30:31], off offset:1152
	global_load_dword v250, v[248:249], off offset:1024
	global_load_dword v251, v[248:249], off offset:1152
	ds_read_b128 v[36:39], v90 offset:2304
	v_lshl_add_u64 v[78:79], s[4:5], 0, v[70:71]
	s_waitcnt lgkmcnt(1)
	v_mfma_f32_16x16x32_bf16 v[62:65], v[14:17], v[2:5], v[10:13]
	s_ashr_i32 s17, s16, 31
	v_mov_b32_e32 v81, v71
	v_cmp_lt_i32_e32 vcc, v84, v85
	ds_read_b128 v[10:13], v90 offset:2368
	v_add3_u32 v159, v87, v76, v88
	s_nop 2
	v_mul_f32_e32 v14, 0x3e000000, v62
	v_mul_f32_e32 v15, 0x3e000000, v63
	v_max3_f32 v35, v35, v14, v15
	v_mul_f32_e32 v40, 0x3e000000, v64
	s_waitcnt lgkmcnt(1)
	v_mfma_f32_16x16x32_bf16 v[14:17], v[36:39], v[6:9], 0
	v_mul_f32_e32 v36, 0x3e000000, v65
	v_max3_f32 v35, v35, v40, v36
	ds_read_b128 v[36:39], v90 offset:4608
	s_waitcnt lgkmcnt(1)
	v_mfma_f32_16x16x32_bf16 v[66:69], v[10:13], v[2:5], v[14:17]
	ds_read_b128 v[10:13], v90 offset:4672
	s_ashr_i32 s19, s18, 31
	s_ashr_i32 s21, s20, 31
	s_ashr_i32 s23, s22, 31
	s_ashr_i32 s25, s24, 31
	s_nop 2
	v_mul_f32_e32 v14, 0x3e000000, v66
	v_mul_f32_e32 v15, 0x3e000000, v67
	v_max3_f32 v35, v35, v14, v15
	s_waitcnt lgkmcnt(1)
	v_mfma_f32_16x16x32_bf16 v[14:17], v[36:39], v[6:9], 0
	v_mul_f32_e32 v40, 0x3e000000, v68
	v_mul_f32_e32 v41, 0x3e000000, v69
	v_max3_f32 v35, v35, v40, v41
	s_waitcnt lgkmcnt(0)
	v_mfma_f32_16x16x32_bf16 v[58:61], v[10:13], v[2:5], v[14:17]
	ds_read_b128 v[36:39], v90 offset:6912
	ds_read_b128 v[40:43], v90 offset:6976
	s_waitcnt vmcnt(7)
	ds_write_b128 v75, v[18:21] offset:18432
	s_waitcnt vmcnt(6)
	ds_write_b128 v75, v[22:25] offset:27648
	s_waitcnt lgkmcnt(0)
	s_nop 0
	v_mul_f32_e32 v10, 0x3e000000, v58
	v_mul_f32_e32 v11, 0x3e000000, v59
	v_max3_f32 v14, v35, v10, v11
	v_mfma_f32_16x16x32_bf16 v[10:13], v[36:39], v[6:9], 0
	v_mul_f32_e32 v15, 0x3e000000, v60
	v_mul_f32_e32 v16, 0x3e000000, v61
	v_max3_f32 v14, v14, v15, v16
	v_mfma_f32_16x16x32_bf16 v[54:57], v[40:43], v[2:5], v[10:13]
	s_barrier
; #define LAS __attribute__((address_space(3)))
; template <bool LOCAL>
; __device__ __forceinline__ void na_unit(const bf16* P, const bf16* VT, bf16* YCAT, const LAS float* rpb_l, LAS bf16* buf, int b, int gr, int hp, int qblk, int tid) {
;     ...
;             } else {
;                 const int cc = c - NLOC;
; #pragma unroll
;                 for (int t4 = 0; t4 < 4; ++t4) {
;                     const LAS bf16* kp = cb + (16 * t4 + fr) * 72 + 8 * fq;
;                     f32x4 acc = {0.f, 0.f, 0.f, 0.f};
;                     acc = __builtin_amdgcn_mfma_f32_16x16x32_bf16(*(const LAS bf16x8*)(kp), qf[0], acc, 0, 0, 0);
;                     acc = __builtin_amdgcn_mfma_f32_16x16x32_bf16(*(const LAS bf16x8*)(kp + 32), qf[1], acc, 0, 0, 0);
; #pragma unroll
;                     for (int e = 0; e < 4; ++e) { acc[e] *= 0.125f; m = fmaxf(m, acc[e]); }
;                     sc[4 * (cc >= 0 ? cc : 0) + t4] = acc; }
;             }
;             if (sidx == NCH - 1) { m = fmaxf(m, __shfl_xor(m, 16)); m = fmaxf(m, __shfl_xor(m, 32)); }
	v_or_b32_e32 v18, 0xc0, v34
	v_mad_i64_i32 v[18:19], s[28:29], v18, s70, v[44:45]
	v_lshl_add_u64 v[18:19], v[18:19], 0, v[70:71]
	s_nop 3
	v_mul_f32_e32 v10, 0x3e000000, v54
	v_mul_f32_e32 v11, 0x3e000000, v55
	v_max3_f32 v14, v14, v10, v11
	ds_read_b128 v[10:13], v90 offset:18432
	v_mul_f32_e32 v15, 0x3e000000, v56
	v_mul_f32_e32 v16, 0x3e000000, v57
	v_max3_f32 v35, v14, v15, v16
	ds_read_b128 v[14:17], v90 offset:18496
	v_lshl_add_u64 v[22:23], v[18:19], 0, s[2:3]
	s_waitcnt lgkmcnt(1)
	v_mfma_f32_16x16x32_bf16 v[10:13], v[10:13], v[6:9], 0
	global_load_dwordx4 v[18:21], v[22:23], off offset:1024
	global_load_dwordx4 v[162:165], v[22:23], off offset:1152
	ds_read_b128 v[22:25], v90 offset:20736
	s_ashr_i32 s27, s26, 31
	s_waitcnt lgkmcnt(1)
	v_mfma_f32_16x16x32_bf16 v[46:49], v[14:17], v[2:5], v[10:13]
	s_nop 2
	ds_read_b128 v[10:13], v90 offset:20800
	s_nop 3
	v_mul_f32_e32 v14, 0x3e000000, v46
	v_mul_f32_e32 v15, 0x3e000000, v47
	v_max3_f32 v34, v35, v14, v15
	v_mul_f32_e32 v35, 0x3e000000, v48
	s_waitcnt lgkmcnt(1)
	v_mfma_f32_16x16x32_bf16 v[14:17], v[22:25], v[6:9], 0
	v_mul_f32_e32 v22, 0x3e000000, v49
	v_max3_f32 v34, v34, v35, v22
	ds_read_b128 v[22:25], v90 offset:23040
	s_waitcnt lgkmcnt(1)
	v_mfma_f32_16x16x32_bf16 v[50:53], v[10:13], v[2:5], v[14:17]
	ds_read_b128 v[10:13], v90 offset:23104
	s_nop 6
	v_mul_f32_e32 v14, 0x3e000000, v50
	v_mul_f32_e32 v15, 0x3e000000, v51
	v_max3_f32 v34, v34, v14, v15
	s_waitcnt lgkmcnt(1)
	v_mfma_f32_16x16x32_bf16 v[14:17], v[22:25], v[6:9], 0
	v_mul_f32_e32 v35, 0x3e000000, v52
	v_mul_f32_e32 v36, 0x3e000000, v53
	v_max3_f32 v38, v34, v35, v36
	s_waitcnt lgkmcnt(0)
	v_mfma_f32_16x16x32_bf16 v[42:45], v[10:13], v[2:5], v[14:17]
	ds_read_b128 v[22:25], v90 offset:25344
	ds_read_b128 v[34:37], v90 offset:25408
	s_waitcnt vmcnt(5)
	ds_write_b128 v75, v[26:29]
	s_waitcnt vmcnt(4)
	ds_write_b128 v75, v[30:33] offset:9216
	s_waitcnt lgkmcnt(0)
	s_nop 0
	v_mul_f32_e32 v10, 0x3e000000, v42
	v_mul_f32_e32 v11, 0x3e000000, v43
	v_max3_f32 v14, v38, v10, v11
	v_mfma_f32_16x16x32_bf16 v[10:13], v[22:25], v[6:9], 0
	v_mul_f32_e32 v15, 0x3e000000, v44
	v_mul_f32_e32 v16, 0x3e000000, v45
	v_max3_f32 v14, v14, v15, v16
	v_mfma_f32_16x16x32_bf16 v[38:41], v[34:37], v[2:5], v[10:13]
	s_barrier
	v_add3_u32 v26, v89, s1, 64
	v_mul_u32_u24_e32 v26, 0x9000, v26
	v_lshl_add_u64 v[22:23], s[16:17], 1, v[78:79]
	s_nop 3
	v_mul_f32_e32 v10, 0x3e000000, v38
	v_mul_f32_e32 v11, 0x3e000000, v39
	v_max3_f32 v10, v14, v10, v11
	v_mul_f32_e32 v11, 0x3e000000, v40
	v_mul_f32_e32 v12, 0x3e000000, v41
	v_max3_f32 v34, v10, v11, v12
	v_or_b32_e32 v10, s1, v89
	v_mul_u32_u24_e32 v14, 0x9000, v10
	ds_read_b128 v[10:13], v90
	v_lshlrev_b32_e32 v70, 1, v14
	ds_read_b128 v[14:17], v90 offset:64
	v_lshlrev_b32_e32 v80, 1, v26
	v_lshl_add_u64 v[24:25], v[22:23], 0, v[70:71]
	v_lshl_add_u64 v[22:23], v[22:23], 0, v[80:81]
	s_waitcnt lgkmcnt(1)
	v_mfma_f32_16x16x32_bf16 v[10:13], v[10:13], v[6:9], 0
	v_lshl_add_u64 v[248:249], v[24:25], 0, 0
	v_lshl_add_u64 v[238:239], v[22:23], 0, 0
	global_load_dwordx4 v[166:169], v[24:25], off
	global_load_dwordx4 v[170:173], v[22:23], off
	global_load_dword v250, v[248:249], off offset:128
	global_load_dword v251, v[238:239], off offset:128
	ds_read_b128 v[22:25], v90 offset:2304
	s_add_i32 s16, s15, s50
	s_waitcnt lgkmcnt(1)
	v_mfma_f32_16x16x32_bf16 v[30:33], v[14:17], v[2:5], v[10:13]
	s_ashr_i32 s17, s16, 31
	s_ashr_i32 s15, s14, 31
	s_ashr_i32 s1, s0, 31
	ds_read_b128 v[10:13], v90 offset:2368
	s_nop 3
	v_mul_f32_e32 v14, 0x3e000000, v30
	v_mul_f32_e32 v15, 0x3e000000, v31
	v_max3_f32 v26, v34, v14, v15
	v_mul_f32_e32 v27, 0x3e000000, v32
	s_waitcnt lgkmcnt(1)
	v_mfma_f32_16x16x32_bf16 v[14:17], v[22:25], v[6:9], 0
	v_mul_f32_e32 v22, 0x3e000000, v33
	v_max3_f32 v26, v26, v27, v22
	ds_read_b128 v[22:25], v90 offset:4608
	s_waitcnt lgkmcnt(1)
	v_mfma_f32_16x16x32_bf16 v[34:37], v[10:13], v[2:5], v[14:17]
	ds_read_b128 v[10:13], v90 offset:4672
	s_nop 6
	v_mul_f32_e32 v14, 0x3e000000, v34
	v_mul_f32_e32 v15, 0x3e000000, v35
	v_max3_f32 v26, v26, v14, v15
	s_waitcnt lgkmcnt(1)
	v_mfma_f32_16x16x32_bf16 v[14:17], v[22:25], v[6:9], 0
	v_mul_f32_e32 v27, 0x3e000000, v36
	v_mul_f32_e32 v28, 0x3e000000, v37
	v_max3_f32 v89, v26, v27, v28
	s_waitcnt lgkmcnt(0)
	v_mfma_f32_16x16x32_bf16 v[26:29], v[10:13], v[2:5], v[14:17]
	ds_read_b128 v[22:25], v90 offset:6912
	ds_read_b128 v[174:177], v90 offset:6976
	s_waitcnt vmcnt(5)
	ds_write_b128 v75, v[18:21] offset:18432
	s_waitcnt vmcnt(4)
	ds_write_b128 v75, v[162:165] offset:27648
	s_waitcnt lgkmcnt(0)
	s_nop 0
	v_mul_f32_e32 v10, 0x3e000000, v26
	v_mul_f32_e32 v11, 0x3e000000, v27
	v_max3_f32 v14, v89, v10, v11
	v_mfma_f32_16x16x32_bf16 v[10:13], v[22:25], v[6:9], 0
	v_mul_f32_e32 v15, 0x3e000000, v28
	v_mul_f32_e32 v16, 0x3e000000, v29
	v_max3_f32 v14, v14, v15, v16
	v_mfma_f32_16x16x32_bf16 v[22:25], v[174:177], v[2:5], v[10:13]
	s_barrier
; #define LAS __attribute__((address_space(3)))
; __device__ __forceinline__ unsigned cvt_pk_bf16(float lo, float hi) { const float __attribute__((ext_vector_type(2))) v = {lo, hi}; return __builtin_bit_cast(unsigned, __builtin_convertvector(v, bf16x2_t)); }
; template <bool LOCAL>
; __device__ __forceinline__ void na_unit(const bf16* P, const bf16* VT, bf16* YCAT, const LAS float* rpb_l, LAS bf16* buf, int b, int gr, int hp, int qblk, int tid) {
;     ...
;             if (sidx == NCH - 1) { m = fmaxf(m, __shfl_xor(m, 16)); m = fmaxf(m, __shfl_xor(m, 32)); }
;         } else {
;             const int c = sidx - NCH;
;             if (LOCAL && c < 8) {
;                 float p[8];
; #pragma unroll
;                 for (int e = 0; e < 4; ++e) { p[e] = __expf(sl[2 * (c < 8 ? c : 0)][e] - m); p[4 + e] = __expf(sl[2 * (c < 8 ? c : 0) + 1][e] - m); }
; #pragma unroll
;                 for (int e = 0; e < 8; ++e) lsum += p[e];
;                 const bf16x8 pf = __builtin_bit_cast(bf16x8, (v4u){pg8::cvt_pk_bf16(p[0], p[1]), pg8::cvt_pk_bf16(p[2], p[3]), pg8::cvt_pk_bf16(p[4], p[5]), pg8::cvt_pk_bf16(p[6], p[7])});
; #pragma unroll
;                 for (int dt = 0; dt < 4; ++dt) { const LAS bf16* vp = cb + (16 * dt + fr) * 72 + kc0 + 4 * fq;
;                     o[dt] = __builtin_amdgcn_mfma_f32_16x16x32_bf16(frag44(vp, vp + 16), pf, o[dt], 0, 0, 0); }
	v_lshl_add_u64 v[18:19], s[16:17], 1, v[78:79]
	v_lshl_add_u64 v[20:21], v[18:19], 0, v[70:71]
	v_lshl_add_u64 v[18:19], v[18:19], 0, v[80:81]
	s_nop 3
	v_mul_f32_e32 v10, 0x3e000000, v22
	v_mul_f32_e32 v11, 0x3e000000, v23
	v_max3_f32 v14, v14, v10, v11
	ds_read_b128 v[10:13], v90 offset:18432
	v_mul_f32_e32 v15, 0x3e000000, v24
	v_mul_f32_e32 v16, 0x3e000000, v25
	v_max3_f32 v89, v14, v15, v16
	ds_read_b128 v[14:17], v90 offset:18496
	s_waitcnt lgkmcnt(1)
	v_mfma_f32_16x16x32_bf16 v[10:13], v[10:13], v[6:9], 0
	v_lshl_add_u64 v[248:249], v[20:21], 0, 0
	v_lshl_add_u64 v[238:239], v[18:19], 0, 0
	global_load_dwordx4 v[162:165], v[20:21], off
	global_load_dwordx4 v[174:177], v[18:19], off
	global_load_dword v250, v[248:249], off offset:128
	global_load_dword v251, v[238:239], off offset:128
	ds_read_b128 v[18:21], v90 offset:20736
	ds_read_b128 v[178:181], v90 offset:23040
	s_waitcnt lgkmcnt(2)
	v_mfma_f32_16x16x32_bf16 v[14:17], v[14:17], v[2:5], v[10:13]
	s_nop 2
	ds_read_b128 v[10:13], v90 offset:20800
	s_waitcnt lgkmcnt(2)
	v_mfma_f32_16x16x32_bf16 v[18:21], v[18:21], v[6:9], 0
	s_nop 1
	v_mul_f32_e32 v133, 0x3e000000, v14
	v_mul_f32_e32 v137, 0x3e000000, v15
	v_max3_f32 v89, v89, v133, v137
	s_waitcnt lgkmcnt(0)
	v_mfma_f32_16x16x32_bf16 v[18:21], v[10:13], v[2:5], v[18:21]
	ds_read_b128 v[10:13], v90 offset:23104
	ds_read_b128 v[182:185], v90 offset:25344
	ds_read_b128 v[186:189], v90 offset:25408
	v_mul_f32_e32 v133, 0x3e000000, v16
	v_mfma_f32_16x16x32_bf16 v[178:181], v[178:181], v[6:9], 0
	v_mul_f32_e32 v137, 0x3e000000, v17
	v_max3_f32 v89, v89, v133, v137
	s_nop 0
	v_mul_f32_e32 v133, 0x3e000000, v18
	s_waitcnt lgkmcnt(1)
	v_mfma_f32_16x16x32_bf16 v[6:9], v[182:185], v[6:9], 0
	v_mul_f32_e32 v137, 0x3e000000, v19
	v_max3_f32 v89, v89, v133, v137
	v_mul_f32_e32 v133, 0x3e000000, v20
	v_mfma_f32_16x16x32_bf16 v[10:13], v[10:13], v[2:5], v[178:181]
	v_mul_f32_e32 v137, 0x3e000000, v21
	v_max3_f32 v89, v89, v133, v137
	s_waitcnt vmcnt(7)
	ds_write_b128 v75, v[166:169]
	s_waitcnt vmcnt(6)
	ds_write_b128 v75, v[170:173] offset:9216
	s_waitcnt lgkmcnt(2)
	v_mfma_f32_16x16x32_bf16 v[2:5], v[186:189], v[2:5], v[6:9]
	v_mul_f32_e32 v90, 0x3e000000, v10
	v_mul_f32_e32 v133, 0x3e000000, v11
	v_max3_f32 v89, v89, v90, v133
	v_mul_f32_e32 v90, 0x3e000000, v12
	v_mul_f32_e32 v133, 0x3e000000, v13
	v_max3_f32 v89, v89, v90, v133
	s_nop 1
	v_mul_f32_e32 v6, 0x3e000000, v2
	v_mul_f32_e32 v7, 0x3e000000, v3
	v_max3_f32 v6, v89, v6, v7
	v_mul_f32_e32 v7, 0x3e000000, v4
	v_mul_f32_e32 v8, 0x3e000000, v5
	v_max3_f32 v6, v6, v7, v8
	v_cndmask_b32_e32 v7, v83, v84, vcc
	v_lshlrev_b32_e32 v89, 2, v7
	ds_bpermute_b32 v7, v89, v6
	v_cmp_lt_i32_e32 vcc, v86, v85
	v_lshl_add_u32 v8, v91, 1, v159
	v_lshl_add_u64 v[186:187], s[14:15], 1, v[78:79]
	v_lshl_add_u64 v[188:189], v[186:187], 0, v[70:71]
	s_waitcnt lgkmcnt(0)
	v_max_f32_e32 v7, v7, v7
	v_max_f32_e32 v6, v6, v7
	v_cndmask_b32_e32 v7, v83, v86, vcc
	v_lshlrev_b32_e32 v90, 2, v7
	ds_bpermute_b32 v7, v90, v6
	v_lshl_add_u64 v[190:191], v[186:187], 0, v[80:81]
	s_waitcnt lgkmcnt(0)
	s_barrier
	v_max_f32_e32 v7, v7, v7
	v_max_f32_e32 v137, v6, v7
	v_sub_f32_e32 v6, v93, v137
	v_mul_f32_e32 v6, 0x3fb8aa3b, v6
	v_exp_f32_e32 v133, v6
	v_sub_f32_e32 v6, v97, v137
	v_mul_f32_e32 v6, 0x3fb8aa3b, v6
	v_exp_f32_e32 v93, v6
	v_sub_f32_e32 v6, v92, v137
	v_mul_f32_e32 v6, 0x3fb8aa3b, v6
	v_exp_f32_e32 v97, v6
	v_sub_f32_e32 v6, v96, v137
	v_mul_f32_e32 v6, 0x3fb8aa3b, v6
	v_exp_f32_e32 v92, v6
	v_sub_f32_e32 v6, v95, v137
	v_mul_f32_e32 v6, 0x3fb8aa3b, v6
	v_exp_f32_e32 v96, v6
	v_sub_f32_e32 v6, v100, v137
	v_mul_f32_e32 v6, 0x3fb8aa3b, v6
	v_exp_f32_e32 v95, v6
	v_sub_f32_e32 v6, v94, v137
	v_mul_f32_e32 v6, 0x3fb8aa3b, v6
	v_exp_f32_e32 v100, v6
	v_sub_f32_e32 v6, v98, v137
	v_mul_f32_e32 v6, 0x3fb8aa3b, v6
	v_exp_f32_e32 v94, v6
	v_add_u32_e32 v7, 0x800, v8
	v_add_u32_e32 v6, 0x1000, v8
	ds_read2_b64 v[166:169], v8 offset1:4
	ds_read2_b64 v[178:181], v7 offset0:32 offset1:36
	ds_read2_b64 v[182:185], v6 offset0:64 offset1:68
	v_lshl_add_u64 v[248:249], v[188:189], 0, 0
	v_lshl_add_u64 v[238:239], v[190:191], 0, 0
	global_load_dwordx4 v[186:189], v[188:189], off
	s_nop 0
	global_load_dwordx4 v[190:193], v[190:191], off
	global_load_dword v250, v[248:249], off offset:128
	global_load_dword v251, v[238:239], off offset:128
	v_sub_f32_e32 v9, v101, v137
	v_mul_f32_e32 v9, 0x3fb8aa3b, v9
	v_add_u32_e32 v161, 0x1800, v8
	v_exp_f32_e32 v87, v9
	v_sub_f32_e32 v9, v106, v137
	ds_read2_b64 v[194:197], v161 offset0:96 offset1:100
	v_mul_f32_e32 v9, 0x3fb8aa3b, v9
	v_exp_f32_e32 v76, v9
	v_sub_f32_e32 v9, v99, v137
	v_mul_f32_e32 v9, 0x3fb8aa3b, v9
	v_exp_f32_e32 v91, v9
	v_sub_f32_e32 v9, v104, v137
	v_mul_f32_e32 v9, 0x3fb8aa3b, v9
	v_exp_f32_e32 v88, v9
	v_sub_f32_e32 v9, v103, v137
	v_mul_f32_e32 v9, 0x3fb8aa3b, v9
	v_exp_f32_e32 v99, v9
	v_sub_f32_e32 v9, v110, v137
	v_cvt_pk_bf16_f32 v170, v133, v97
	v_cvt_pk_bf16_f32 v171, v96, v100
	v_cvt_pk_bf16_f32 v172, v93, v92
	v_cvt_pk_bf16_f32 v173, v95, v94
	s_waitcnt vmcnt(7)
	ds_write_b128 v75, v[162:165] offset:18432
	s_waitcnt vmcnt(6)
	ds_write_b128 v75, v[174:177] offset:27648
	v_mul_f32_e32 v9, 0x3fb8aa3b, v9
	v_add_u32_e32 v163, 0x4800, v8
	v_add_u32_e32 v162, 0x5000, v8
	s_waitcnt lgkmcnt(5)
	v_mfma_f32_16x16x32_bf16 v[166:169], v[166:169], v[170:173], 0
	s_waitcnt lgkmcnt(0)
	s_barrier
; #define LAS __attribute__((address_space(3)))
; __device__ __forceinline__ unsigned cvt_pk_bf16(float lo, float hi) { const float __attribute__((ext_vector_type(2))) v = {lo, hi}; return __builtin_bit_cast(unsigned, __builtin_convertvector(v, bf16x2_t)); }
; template <bool LOCAL>
; __device__ __forceinline__ void na_unit(const bf16* P, const bf16* VT, bf16* YCAT, const LAS float* rpb_l, LAS bf16* buf, int b, int gr, int hp, int qblk, int tid) {
;     ...
;         } else {
;             const int c = sidx - NCH;
;             if (LOCAL && c < 8) {
;                 float p[8];
; #pragma unroll
;                 for (int e = 0; e < 4; ++e) { p[e] = __expf(sl[2 * (c < 8 ? c : 0)][e] - m); p[4 + e] = __expf(sl[2 * (c < 8 ? c : 0) + 1][e] - m); }
; #pragma unroll
;                 for (int e = 0; e < 8; ++e) lsum += p[e];
;                 const bf16x8 pf = __builtin_bit_cast(bf16x8, (v4u){pg8::cvt_pk_bf16(p[0], p[1]), pg8::cvt_pk_bf16(p[2], p[3]), pg8::cvt_pk_bf16(p[4], p[5]), pg8::cvt_pk_bf16(p[6], p[7])});
; #pragma unroll
;                 for (int dt = 0; dt < 4; ++dt) { const LAS bf16* vp = cb + (16 * dt + fr) * 72 + kc0 + 4 * fq;
;                     o[dt] = __builtin_amdgcn_mfma_f32_16x16x32_bf16(frag44(vp, vp + 16), pf, o[dt], 0, 0, 0); }
	v_mfma_f32_16x16x32_bf16 v[178:181], v[178:181], v[170:173], 0
	v_exp_f32_e32 v98, v9
	v_sub_f32_e32 v9, v102, v137
	ds_read2_b64 v[174:177], v163 offset1:4
	v_mfma_f32_16x16x32_bf16 v[182:185], v[182:185], v[170:173], 0
	v_mul_f32_e32 v9, 0x3fb8aa3b, v9
	v_exp_f32_e32 v101, v9
	v_sub_f32_e32 v9, v108, v137
	v_mfma_f32_16x16x32_bf16 v[170:173], v[194:197], v[170:173], 0
	ds_read2_b64 v[194:197], v162 offset0:32 offset1:36
	v_mul_f32_e32 v9, 0x3fb8aa3b, v9
	v_exp_f32_e32 v102, v9
	v_lshl_add_u64 v[164:165], s[0:1], 1, v[78:79]
	v_cvt_pk_bf16_f32 v198, v87, v91
	v_cvt_pk_bf16_f32 v199, v99, v101
	v_cvt_pk_bf16_f32 v200, v76, v88
	v_cvt_pk_bf16_f32 v201, v98, v102
	v_lshl_add_u64 v[202:203], v[164:165], 0, v[70:71]
	v_lshl_add_u64 v[204:205], v[164:165], 0, v[80:81]
	v_add_u32_e32 v164, 0x5800, v8
	s_waitcnt lgkmcnt(1)
	v_mfma_f32_16x16x32_bf16 v[166:169], v[174:177], v[198:201], v[166:169]
	v_sub_f32_e32 v9, v107, v137
	v_mul_f32_e32 v9, 0x3fb8aa3b, v9
	v_add_u32_e32 v165, 0x6000, v8
	s_waitcnt lgkmcnt(0)
	v_mfma_f32_16x16x32_bf16 v[174:177], v[194:197], v[198:201], v[178:181]
	v_exp_f32_e32 v104, v9
	v_sub_f32_e32 v9, v114, v137
	v_mul_f32_e32 v9, 0x3fb8aa3b, v9
	ds_read2_b64 v[178:181], v164 offset0:64 offset1:68
	v_lshl_add_u64 v[248:249], v[202:203], 0, 0
	v_lshl_add_u64 v[238:239], v[204:205], 0, 0
	global_load_dwordx4 v[194:197], v[202:203], off
	s_nop 0
	global_load_dwordx4 v[202:205], v[204:205], off
	global_load_dword v250, v[248:249], off offset:128
	global_load_dword v251, v[238:239], off offset:128
	s_waitcnt lgkmcnt(0)
	v_mfma_f32_16x16x32_bf16 v[178:181], v[178:181], v[198:201], v[182:185]
	s_nop 2
	ds_read2_b64 v[182:185], v165 offset0:96 offset1:100
	v_exp_f32_e32 v103, v9
	v_sub_f32_e32 v9, v105, v137
	v_mul_f32_e32 v9, 0x3fb8aa3b, v9
	v_exp_f32_e32 v106, v9
	v_sub_f32_e32 v9, v112, v137
	v_mul_f32_e32 v9, 0x3fb8aa3b, v9
	v_exp_f32_e32 v105, v9
	v_sub_f32_e32 v9, v111, v137
	v_mul_f32_e32 v9, 0x3fb8aa3b, v9
	v_exp_f32_e32 v108, v9
	v_sub_f32_e32 v9, v117, v137
	v_mul_f32_e32 v9, 0x3fb8aa3b, v9
	s_waitcnt lgkmcnt(0)
	v_mfma_f32_16x16x32_bf16 v[170:173], v[182:185], v[198:201], v[170:173]
	s_waitcnt vmcnt(7)
	ds_write_b128 v75, v[186:189]
	s_waitcnt vmcnt(6)
	ds_write_b128 v75, v[190:193] offset:9216
	s_waitcnt lgkmcnt(0)
	s_barrier
	v_exp_f32_e32 v107, v9
	v_sub_f32_e32 v9, v109, v137
	ds_read2_b64 v[182:185], v8 offset1:4
	ds_read2_b64 v[186:189], v7 offset0:32 offset1:36
	v_mul_f32_e32 v9, 0x3fb8aa3b, v9
	v_exp_f32_e32 v109, v9
	v_sub_f32_e32 v9, v113, v137
	v_mul_f32_e32 v9, 0x3fb8aa3b, v9
	v_exp_f32_e32 v110, v9
	v_lshl_add_u64 v[198:199], s[18:19], 1, v[78:79]
	v_cvt_pk_bf16_f32 v190, v104, v106
	v_cvt_pk_bf16_f32 v191, v108, v109
	v_cvt_pk_bf16_f32 v192, v103, v105
	v_cvt_pk_bf16_f32 v193, v107, v110
	v_lshl_add_u64 v[112:113], v[198:199], 0, v[70:71]
	v_lshl_add_u64 v[198:199], v[198:199], 0, v[80:81]
	s_waitcnt lgkmcnt(1)
	v_mfma_f32_16x16x32_bf16 v[166:169], v[182:185], v[190:193], v[166:169]
	ds_read2_b64 v[182:185], v6 offset0:64 offset1:68
	v_sub_f32_e32 v9, v116, v137
	v_mul_f32_e32 v9, 0x3fb8aa3b, v9
	s_waitcnt lgkmcnt(1)
	v_mfma_f32_16x16x32_bf16 v[174:177], v[186:189], v[190:193], v[174:177]
	v_lshl_add_u64 v[248:249], v[112:113], 0, 0
	v_lshl_add_u64 v[238:239], v[198:199], 0, 0
	global_load_dwordx4 v[186:189], v[112:113], off
	s_nop 0
	global_load_dwordx4 v[198:201], v[198:199], off
	global_load_dword v250, v[248:249], off offset:128
	global_load_dword v251, v[238:239], off offset:128
	v_exp_f32_e32 v112, v9
	v_sub_f32_e32 v9, v122, v137
	s_waitcnt lgkmcnt(0)
	v_mfma_f32_16x16x32_bf16 v[178:181], v[182:185], v[190:193], v[178:181]
	ds_read2_b64 v[182:185], v161 offset0:96 offset1:100
	v_mul_f32_e32 v9, 0x3fb8aa3b, v9
	v_exp_f32_e32 v111, v9
	v_sub_f32_e32 v9, v115, v137
	v_mul_f32_e32 v9, 0x3fb8aa3b, v9
	v_exp_f32_e32 v114, v9
	v_sub_f32_e32 v9, v120, v137
	v_mul_f32_e32 v9, 0x3fb8aa3b, v9
	v_exp_f32_e32 v113, v9
	v_sub_f32_e32 v9, v119, v137
	v_mul_f32_e32 v9, 0x3fb8aa3b, v9
	v_exp_f32_e32 v116, v9
	v_sub_f32_e32 v9, v125, v137
	v_mul_f32_e32 v9, 0x3fb8aa3b, v9
	s_waitcnt lgkmcnt(0)
	v_mfma_f32_16x16x32_bf16 v[170:173], v[182:185], v[190:193], v[170:173]
	s_waitcnt vmcnt(7)
	ds_write_b128 v75, v[194:197] offset:18432
	s_waitcnt vmcnt(6)
	ds_write_b128 v75, v[202:205] offset:27648
	s_waitcnt lgkmcnt(0)
	s_barrier
	v_exp_f32_e32 v115, v9
	v_sub_f32_e32 v9, v118, v137
	ds_read2_b64 v[182:185], v163 offset1:4
	v_mul_f32_e32 v9, 0x3fb8aa3b, v9
	v_exp_f32_e32 v117, v9
	v_sub_f32_e32 v9, v121, v137
	v_mul_f32_e32 v9, 0x3fb8aa3b, v9
	v_exp_f32_e32 v118, v9
	v_lshl_add_u64 v[202:203], s[20:21], 1, v[78:79]
	v_lshl_add_u64 v[204:205], v[202:203], 0, v[70:71]
	ds_read2_b64 v[190:193], v162 offset0:32 offset1:36
	v_cvt_pk_bf16_f32 v194, v112, v114
	v_cvt_pk_bf16_f32 v195, v116, v117
	v_cvt_pk_bf16_f32 v196, v111, v113
	v_cvt_pk_bf16_f32 v197, v115, v118
	v_lshl_add_u64 v[120:121], v[202:203], 0, v[80:81]
	v_sub_f32_e32 v9, v124, v137
	s_waitcnt lgkmcnt(1)
	v_mfma_f32_16x16x32_bf16 v[166:169], v[182:185], v[194:197], v[166:169]
	v_lshl_add_u64 v[248:249], v[204:205], 0, 0
	v_lshl_add_u64 v[238:239], v[120:121], 0, 0
	global_load_dwordx4 v[182:185], v[204:205], off
	s_nop 0
	global_load_dwordx4 v[202:205], v[120:121], off
	global_load_dword v250, v[248:249], off offset:128
	global_load_dword v251, v[238:239], off offset:128
	v_mul_f32_e32 v9, 0x3fb8aa3b, v9
	v_exp_f32_e32 v120, v9
	s_waitcnt lgkmcnt(0)
	v_mfma_f32_16x16x32_bf16 v[174:177], v[190:193], v[194:197], v[174:177]
	ds_read2_b64 v[190:193], v164 offset0:64 offset1:68
	v_sub_f32_e32 v9, v130, v137
	v_mul_f32_e32 v9, 0x3fb8aa3b, v9
	s_waitcnt lgkmcnt(0)
	v_mfma_f32_16x16x32_bf16 v[178:181], v[190:193], v[194:197], v[178:181]
	ds_read2_b64 v[190:193], v165 offset0:96 offset1:100
	v_exp_f32_e32 v119, v9
	v_sub_f32_e32 v9, v123, v137
	v_mul_f32_e32 v9, 0x3fb8aa3b, v9
	v_exp_f32_e32 v122, v9
	v_sub_f32_e32 v9, v128, v137
	v_mul_f32_e32 v9, 0x3fb8aa3b, v9
	v_exp_f32_e32 v121, v9
	v_sub_f32_e32 v9, v127, v137
	v_mul_f32_e32 v9, 0x3fb8aa3b, v9
	v_exp_f32_e32 v124, v9
	v_sub_f32_e32 v9, v134, v137
	v_mul_f32_e32 v9, 0x3fb8aa3b, v9
	s_waitcnt lgkmcnt(0)
	v_mfma_f32_16x16x32_bf16 v[170:173], v[190:193], v[194:197], v[170:173]
	s_waitcnt vmcnt(7)
	ds_write_b128 v75, v[186:189]
	s_waitcnt vmcnt(6)
	ds_write_b128 v75, v[198:201] offset:9216
	s_waitcnt lgkmcnt(0)
	s_barrier
; #define LAS __attribute__((address_space(3)))
; __device__ __forceinline__ unsigned cvt_pk_bf16(float lo, float hi) { const float __attribute__((ext_vector_type(2))) v = {lo, hi}; return __builtin_bit_cast(unsigned, __builtin_convertvector(v, bf16x2_t)); }
; #define NA_STORE(sidx) do { LAS bf16* d_ = buf + ((sidx) & 1) * 9216; _Pragma("unroll") for (int q_ = 0; q_ < 2; ++q_) *(LAS v4u*)(d_ + q_ * 4608 + lrow * 72 + lseg * 8) = ld[(sidx) & 1][q_]; } while (0)
; template <bool LOCAL>
; __device__ __forceinline__ void na_unit(const bf16* P, const bf16* VT, bf16* YCAT, const LAS float* rpb_l, LAS bf16* buf, int b, int gr, int hp, int qblk, int tid) {
;     ...
;             if (LOCAL && c < 8) {
;                 float p[8];
; #pragma unroll
;                 for (int e = 0; e < 4; ++e) { p[e] = __expf(sl[2 * (c < 8 ? c : 0)][e] - m); p[4 + e] = __expf(sl[2 * (c < 8 ? c : 0) + 1][e] - m); }
; #pragma unroll
;                 for (int e = 0; e < 8; ++e) lsum += p[e];
;                 const bf16x8 pf = __builtin_bit_cast(bf16x8, (v4u){pg8::cvt_pk_bf16(p[0], p[1]), pg8::cvt_pk_bf16(p[2], p[3]), pg8::cvt_pk_bf16(p[4], p[5]), pg8::cvt_pk_bf16(p[6], p[7])});
; #pragma unroll
;                 for (int dt = 0; dt < 4; ++dt) { const LAS bf16* vp = cb + (16 * dt + fr) * 72 + kc0 + 4 * fq;
;                     o[dt] = __builtin_amdgcn_mfma_f32_16x16x32_bf16(frag44(vp, vp + 16), pf, o[dt], 0, 0, 0); }
;     ...
;         if (sidx + 1 < 2 * NCH) NA_STORE(sidx + 1);
	v_exp_f32_e32 v123, v9
	v_sub_f32_e32 v9, v126, v137
	ds_read2_b64 v[186:189], v8 offset1:4
	ds_read2_b64 v[190:193], v7 offset0:32 offset1:36
	v_mul_f32_e32 v9, 0x3fb8aa3b, v9
	v_exp_f32_e32 v125, v9
	v_sub_f32_e32 v9, v129, v137
	v_mul_f32_e32 v9, 0x3fb8aa3b, v9
	v_exp_f32_e32 v126, v9
	v_lshl_add_u64 v[198:199], s[22:23], 1, v[78:79]
	v_cvt_pk_bf16_f32 v194, v120, v122
	v_cvt_pk_bf16_f32 v195, v124, v125
	v_cvt_pk_bf16_f32 v196, v119, v121
	v_cvt_pk_bf16_f32 v197, v123, v126
	v_lshl_add_u64 v[128:129], v[198:199], 0, v[70:71]
	v_lshl_add_u64 v[198:199], v[198:199], 0, v[80:81]
	s_waitcnt lgkmcnt(1)
	v_mfma_f32_16x16x32_bf16 v[166:169], v[186:189], v[194:197], v[166:169]
	ds_read2_b64 v[186:189], v6 offset0:64 offset1:68
	v_sub_f32_e32 v9, v132, v137
	v_mul_f32_e32 v9, 0x3fb8aa3b, v9
	s_waitcnt lgkmcnt(1)
	v_mfma_f32_16x16x32_bf16 v[174:177], v[190:193], v[194:197], v[174:177]
	v_lshl_add_u64 v[248:249], v[128:129], 0, 0
	v_lshl_add_u64 v[238:239], v[198:199], 0, 0
	global_load_dwordx4 v[190:193], v[128:129], off
	s_nop 0
	global_load_dwordx4 v[198:201], v[198:199], off
	global_load_dword v250, v[248:249], off offset:128
	global_load_dword v251, v[238:239], off offset:128
	v_exp_f32_e32 v128, v9
	v_sub_f32_e32 v9, v140, v137
	v_mul_f32_e32 v9, 0x3fb8aa3b, v9
	v_exp_f32_e32 v127, v9
	v_sub_f32_e32 v9, v131, v137
	v_mul_f32_e32 v9, 0x3fb8aa3b, v9
	v_exp_f32_e32 v130, v9
	v_sub_f32_e32 v9, v138, v137
	v_mul_f32_e32 v9, 0x3fb8aa3b, v9
	v_exp_f32_e32 v129, v9
	v_sub_f32_e32 v9, v136, v137
	v_mul_f32_e32 v9, 0x3fb8aa3b, v9
	v_exp_f32_e32 v132, v9
	v_sub_f32_e32 v9, v143, v137
	s_waitcnt lgkmcnt(0)
	v_mfma_f32_16x16x32_bf16 v[178:181], v[186:189], v[194:197], v[178:181]
	ds_read2_b64 v[186:189], v161 offset0:96 offset1:100
	v_mul_f32_e32 v9, 0x3fb8aa3b, v9
	s_waitcnt vmcnt(7)
	ds_write_b128 v75, v[182:185] offset:18432
	s_waitcnt vmcnt(6)
	ds_write_b128 v75, v[202:205] offset:27648
	s_waitcnt lgkmcnt(0)
	s_barrier
	v_exp_f32_e32 v131, v9
	v_sub_f32_e32 v9, v135, v137
	ds_read2_b64 v[182:185], v163 offset1:4
	v_mul_f32_e32 v9, 0x3fb8aa3b, v9
	v_exp_f32_e32 v134, v9
	v_sub_f32_e32 v9, v139, v137
	v_mul_f32_e32 v9, 0x3fb8aa3b, v9
	v_exp_f32_e32 v135, v9
	v_lshl_add_u64 v[202:203], s[24:25], 1, v[78:79]
	v_mfma_f32_16x16x32_bf16 v[170:173], v[186:189], v[194:197], v[170:173]
	v_lshl_add_u64 v[204:205], v[202:203], 0, v[70:71]
	ds_read2_b64 v[186:189], v162 offset0:32 offset1:36
	v_cvt_pk_bf16_f32 v194, v128, v130
	v_cvt_pk_bf16_f32 v195, v132, v134
	v_cvt_pk_bf16_f32 v196, v127, v129
	v_cvt_pk_bf16_f32 v197, v131, v135
	v_lshl_add_u64 v[138:139], v[202:203], 0, v[80:81]
	v_sub_f32_e32 v9, v142, v137
	s_waitcnt lgkmcnt(1)
	v_mfma_f32_16x16x32_bf16 v[166:169], v[182:185], v[194:197], v[166:169]
	global_load_dwordx4 v[182:185], v[204:205], off
	s_nop 0
	global_load_dwordx4 v[202:205], v[138:139], off
	v_mul_f32_e32 v9, 0x3fb8aa3b, v9
	v_exp_f32_e32 v138, v9
	s_waitcnt lgkmcnt(0)
	v_mfma_f32_16x16x32_bf16 v[174:177], v[186:189], v[194:197], v[174:177]
	ds_read2_b64 v[186:189], v164 offset0:64 offset1:68
	v_sub_f32_e32 v9, v150, v137
	v_mul_f32_e32 v9, 0x3fb8aa3b, v9
	s_waitcnt lgkmcnt(0)
	v_mfma_f32_16x16x32_bf16 v[178:181], v[186:189], v[194:197], v[178:181]
	ds_read2_b64 v[186:189], v165 offset0:96 offset1:100
	v_exp_f32_e32 v136, v9
	v_sub_f32_e32 v9, v141, v137
	v_mul_f32_e32 v9, 0x3fb8aa3b, v9
	v_exp_f32_e32 v140, v9
	v_sub_f32_e32 v9, v148, v137
	v_mul_f32_e32 v9, 0x3fb8aa3b, v9
	v_exp_f32_e32 v139, v9
	v_sub_f32_e32 v9, v145, v137
	v_mul_f32_e32 v9, 0x3fb8aa3b, v9
	s_waitcnt lgkmcnt(0)
	v_mfma_f32_16x16x32_bf16 v[170:173], v[186:189], v[194:197], v[170:173]
	s_waitcnt vmcnt(5)
	ds_write_b128 v75, v[190:193]
	s_waitcnt vmcnt(4)
	ds_write_b128 v75, v[198:201] offset:9216
	s_waitcnt lgkmcnt(0)
	s_barrier
	v_exp_f32_e32 v142, v9
	v_sub_f32_e32 v9, v153, v137
	ds_read2_b64 v[186:189], v8 offset1:4
	v_mul_f32_e32 v9, 0x3fb8aa3b, v9
	ds_read2_b64 v[194:197], v7 offset0:32 offset1:36
	v_exp_f32_e32 v141, v9
	v_sub_f32_e32 v9, v144, v137
	v_sub_f32_e32 v8, v149, v137
	v_mul_f32_e32 v9, 0x3fb8aa3b, v9
	v_mul_f32_e32 v8, 0x3fb8aa3b, v8
	v_exp_f32_e32 v143, v9
	v_exp_f32_e32 v144, v8
	v_cvt_pk_bf16_f32 v190, v138, v140
	v_cvt_pk_bf16_f32 v192, v136, v139
	v_cvt_pk_bf16_f32 v191, v142, v143
	v_cvt_pk_bf16_f32 v193, v141, v144
	v_lshl_add_u64 v[8:9], s[26:27], 1, v[78:79]
	v_sub_f32_e32 v148, v154, v137
	s_waitcnt lgkmcnt(1)
	v_mfma_f32_16x16x32_bf16 v[166:169], v[186:189], v[190:193], v[166:169]
	ds_read2_b64 v[186:189], v6 offset0:64 offset1:68
	v_lshl_add_u64 v[6:7], v[8:9], 0, v[70:71]
	v_lshl_add_u64 v[8:9], v[8:9], 0, v[80:81]
	s_waitcnt lgkmcnt(1)
	v_mfma_f32_16x16x32_bf16 v[174:177], v[194:197], v[190:193], v[174:177]
	v_lshl_add_u64 v[248:249], v[6:7], 0, 0
	v_lshl_add_u64 v[238:239], v[8:9], 0, 0
	global_load_dwordx4 v[194:197], v[6:7], off
	global_load_dwordx4 v[198:201], v[8:9], off
	global_load_dword v250, v[248:249], off offset:128
	global_load_dword v251, v[238:239], off offset:128
	ds_read2_b64 v[78:81], v161 offset0:96 offset1:100
	s_waitcnt vmcnt(5)
	ds_write_b128 v75, v[182:185] offset:18432
	s_waitcnt vmcnt(4)
	ds_write_b128 v75, v[202:205] offset:27648
	s_waitcnt lgkmcnt(2)
	v_mfma_f32_16x16x32_bf16 v[170:173], v[78:81], v[190:193], v[170:173]
	s_waitcnt lgkmcnt(0)
	s_barrier
; #define LAS __attribute__((address_space(3)))
; __device__ __forceinline__ unsigned cvt_pk_bf16(float lo, float hi) { const float __attribute__((ext_vector_type(2))) v = {lo, hi}; return __builtin_bit_cast(unsigned, __builtin_convertvector(v, bf16x2_t)); }
; template <bool LOCAL>
; __device__ __forceinline__ void na_unit(const bf16* P, const bf16* VT, bf16* YCAT, const LAS float* rpb_l, LAS bf16* buf, int b, int gr, int hp, int qblk, int tid) {
;     ...
;             if (LOCAL && c < 8) {
;                 float p[8];
; #pragma unroll
;                 for (int e = 0; e < 4; ++e) { p[e] = __expf(sl[2 * (c < 8 ? c : 0)][e] - m); p[4 + e] = __expf(sl[2 * (c < 8 ? c : 0) + 1][e] - m); }
; #pragma unroll
;                 for (int e = 0; e < 8; ++e) lsum += p[e];
;                 const bf16x8 pf = __builtin_bit_cast(bf16x8, (v4u){pg8::cvt_pk_bf16(p[0], p[1]), pg8::cvt_pk_bf16(p[2], p[3]), pg8::cvt_pk_bf16(p[4], p[5]), pg8::cvt_pk_bf16(p[6], p[7])});
; #pragma unroll
;                 for (int dt = 0; dt < 4; ++dt) { const LAS bf16* vp = cb + (16 * dt + fr) * 72 + kc0 + 4 * fq;
;                     o[dt] = __builtin_amdgcn_mfma_f32_16x16x32_bf16(frag44(vp, vp + 16), pf, o[dt], 0, 0, 0); }
;             } else {
;                 const int cc = c - NLOC;
; #pragma unroll
;                 for (int p2 = 0; p2 < 2; ++p2) {
;                     float p[8];
; #pragma unroll
;                     for (int e = 0; e < 4; ++e) { p[e] = __expf(sc[4 * (cc >= 0 ? cc : 0) + 2 * p2][e] - m); p[4 + e] = __expf(sc[4 * (cc >= 0 ? cc : 0) + 2 * p2 + 1][e] - m); }
; #pragma unroll
;                     for (int e = 0; e < 8; ++e) lsum += p[e];
;                     const bf16x8 pf = __builtin_bit_cast(bf16x8, (v4u){pg8::cvt_pk_bf16(p[0], p[1]), pg8::cvt_pk_bf16(p[2], p[3]), pg8::cvt_pk_bf16(p[4], p[5]), pg8::cvt_pk_bf16(p[6], p[7])});
; #pragma unroll
;                     for (int dt = 0; dt < 4; ++dt) { const LAS bf16* vp = cb + (16 * dt + fr) * 72 + 32 * p2 + 4 * fq;
;                         o[dt] = __builtin_amdgcn_mfma_f32_16x16x32_bf16(frag44(vp, vp + 16), pf, o[dt], 0, 0, 0); }
	v_sub_f32_e32 v70, v152, v137
	v_sub_f32_e32 v79, v151, v137
	v_sub_f32_e32 v81, v155, v137
	ds_read2_b64 v[150:153], v163 offset1:4
	v_mul_f32_e32 v70, 0x3fb8aa3b, v70
	v_mul_f32_e32 v79, 0x3fb8aa3b, v79
	v_mul_f32_e32 v81, 0x3fb8aa3b, v81
	v_mul_f32_e32 v148, 0x3fb8aa3b, v148
	v_exp_f32_e32 v78, v70
	v_sub_f32_e32 v70, v158, v137
	v_exp_f32_e32 v80, v79
	v_sub_f32_e32 v79, v156, v137
	v_exp_f32_e32 v145, v81
	v_sub_f32_e32 v81, v160, v137
	v_exp_f32_e32 v149, v148
	v_sub_f32_e32 v148, v157, v137
	v_mul_f32_e32 v70, 0x3fb8aa3b, v70
	v_mul_f32_e32 v79, 0x3fb8aa3b, v79
	v_mul_f32_e32 v81, 0x3fb8aa3b, v81
	v_mul_f32_e32 v148, 0x3fb8aa3b, v148
	v_exp_f32_e32 v70, v70
	v_exp_f32_e32 v79, v79
	v_exp_f32_e32 v81, v81
	v_exp_f32_e32 v148, v148
	v_cvt_pk_bf16_f32 v154, v78, v80
	v_cvt_pk_bf16_f32 v155, v145, v149
	v_cvt_pk_bf16_f32 v156, v70, v79
	v_cvt_pk_bf16_f32 v157, v81, v148
	v_mfma_f32_16x16x32_bf16 v[178:181], v[186:189], v[190:193], v[178:181]
	v_fma_f32 v62, v62, s72, -v137
	v_fma_f32 v63, v63, s72, -v137
	v_fma_f32 v64, v64, s72, -v137
	s_waitcnt lgkmcnt(0)
	v_mfma_f32_16x16x32_bf16 v[166:169], v[150:153], v[154:157], v[166:169]
	ds_read2_b64 v[150:153], v162 offset0:32 offset1:36
	v_fma_f32 v65, v65, s72, -v137
	v_mul_f32_e32 v62, 0x3fb8aa3b, v62
	s_waitcnt lgkmcnt(0)
	v_mfma_f32_16x16x32_bf16 v[160:163], v[150:153], v[154:157], v[174:177]
	ds_read2_b64 v[150:153], v164 offset0:64 offset1:68
	v_mul_f32_e32 v63, 0x3fb8aa3b, v63
	v_mul_f32_e32 v64, 0x3fb8aa3b, v64
	s_waitcnt lgkmcnt(0)
	v_mfma_f32_16x16x32_bf16 v[174:177], v[150:153], v[154:157], v[178:181]
	ds_read2_b64 v[150:153], v165 offset0:96 offset1:100
	s_nop 1
	v_lshl_add_u64 v[248:249], v[6:7], 0, 0
	v_lshl_add_u64 v[238:239], v[8:9], 0, 0
	global_load_dwordx4 v[178:181], v[6:7], off offset:128
	global_load_dwordx4 v[182:185], v[8:9], off offset:128
	global_load_dword v250, v[248:249], off offset:256
	global_load_dword v251, v[238:239], off offset:256
	s_waitcnt vmcnt(7)
	ds_write_b128 v75, v[194:197]
	s_waitcnt vmcnt(6)
	ds_write_b128 v75, v[198:201] offset:9216
	s_waitcnt lgkmcnt(2)
	v_mfma_f32_16x16x32_bf16 v[152:155], v[150:153], v[154:157], v[170:173]
	s_waitcnt lgkmcnt(0)
	s_barrier
	s_nop 0
	ds_read2_b64 v[170:173], v159 offset1:4
	v_mul_f32_e32 v65, 0x3fb8aa3b, v65
	v_exp_f32_e32 v150, v62
	v_fma_f32 v62, v66, s72, -v137
	v_exp_f32_e32 v66, v63
	v_fma_f32 v63, v67, s72, -v137
	v_exp_f32_e32 v67, v64
	v_fma_f32 v64, v68, s72, -v137
	v_exp_f32_e32 v68, v65
	v_fma_f32 v65, v69, s72, -v137
	v_mul_f32_e32 v62, 0x3fb8aa3b, v62
	v_mul_f32_e32 v63, 0x3fb8aa3b, v63
	v_mul_f32_e32 v64, 0x3fb8aa3b, v64
	v_mul_f32_e32 v65, 0x3fb8aa3b, v65
	v_exp_f32_e32 v62, v62
	v_exp_f32_e32 v63, v63
	v_exp_f32_e32 v64, v64
	v_exp_f32_e32 v65, v65
	v_cvt_pk_bf16_f32 v186, v150, v66
	v_cvt_pk_bf16_f32 v187, v67, v68
	v_cvt_pk_bf16_f32 v188, v62, v63
	v_cvt_pk_bf16_f32 v189, v64, v65
	v_add_u32_e32 v151, 0x800, v159
	v_add_u32_e32 v156, 0x1000, v159
	s_waitcnt lgkmcnt(0)
	v_mfma_f32_16x16x32_bf16 v[164:167], v[170:173], v[186:189], v[166:169]
	v_add_u32_e32 v157, 0x1800, v159
	v_fma_f32 v58, v58, s72, -v137
	v_fma_f32 v54, v54, s72, -v137
	ds_read2_b64 v[168:171], v151 offset0:32 offset1:36
	s_waitcnt lgkmcnt(0)
	v_mfma_f32_16x16x32_bf16 v[160:163], v[168:171], v[186:189], v[160:163]
	ds_read2_b64 v[168:171], v156 offset0:64 offset1:68
	v_fma_f32 v59, v59, s72, -v137
	v_fma_f32 v55, v55, s72, -v137
	s_waitcnt lgkmcnt(0)
	v_mfma_f32_16x16x32_bf16 v[168:171], v[168:171], v[186:189], v[174:177]
	s_nop 2
	ds_read2_b64 v[172:175], v157 offset0:96 offset1:100
	v_fma_f32 v60, v60, s72, -v137
	v_fma_f32 v56, v56, s72, -v137
	s_waitcnt lgkmcnt(0)
	v_mfma_f32_16x16x32_bf16 v[152:155], v[172:175], v[186:189], v[152:155]
	ds_read2_b64 v[172:175], v159 offset0:8 offset1:12
	v_fma_f32 v61, v61, s72, -v137
	v_fma_f32 v57, v57, s72, -v137
	v_mul_f32_e32 v58, 0x3fb8aa3b, v58
	v_mul_f32_e32 v54, 0x3fb8aa3b, v54
	v_mul_f32_e32 v59, 0x3fb8aa3b, v59
	v_mul_f32_e32 v55, 0x3fb8aa3b, v55
	v_mul_f32_e32 v60, 0x3fb8aa3b, v60
	v_mul_f32_e32 v56, 0x3fb8aa3b, v56
	v_mul_f32_e32 v61, 0x3fb8aa3b, v61
	v_mul_f32_e32 v57, 0x3fb8aa3b, v57
	v_exp_f32_e32 v58, v58
	v_exp_f32_e32 v54, v54
	v_exp_f32_e32 v59, v59
	v_exp_f32_e32 v55, v55
	v_exp_f32_e32 v60, v60
	v_exp_f32_e32 v56, v56
	v_exp_f32_e32 v61, v61
	v_exp_f32_e32 v57, v57
	v_cvt_pk_bf16_f32 v186, v58, v59
	v_cvt_pk_bf16_f32 v188, v54, v55
	v_cvt_pk_bf16_f32 v187, v60, v61
	v_cvt_pk_bf16_f32 v189, v56, v57
	v_fma_f32 v46, v46, s72, -v137
	v_fma_f32 v47, v47, s72, -v137
	s_waitcnt lgkmcnt(0)
	v_mfma_f32_16x16x32_bf16 v[164:167], v[172:175], v[186:189], v[164:167]
	ds_read2_b64 v[172:175], v151 offset0:40 offset1:44
	v_fma_f32 v48, v48, s72, -v137
	v_mul_f32_e32 v46, 0x3fb8aa3b, v46
	s_waitcnt lgkmcnt(0)
	v_mfma_f32_16x16x32_bf16 v[160:163], v[172:175], v[186:189], v[160:163]
	ds_read2_b64 v[172:175], v156 offset0:72 offset1:76
	v_mul_f32_e32 v47, 0x3fb8aa3b, v47
	v_mul_f32_e32 v48, 0x3fb8aa3b, v48
	s_waitcnt lgkmcnt(0)
	v_mfma_f32_16x16x32_bf16 v[168:171], v[172:175], v[186:189], v[168:171]
	ds_read2_b64 v[172:175], v157 offset0:104 offset1:108
	v_exp_f32_e32 v69, v46
	v_fma_f32 v46, v50, s72, -v137
	v_exp_f32_e32 v50, v47
	v_fma_f32 v47, v51, s72, -v137
	v_exp_f32_e32 v51, v48
	v_fma_f32 v48, v52, s72, -v137
	v_add_u32_e32 v52, 0x4800, v159
	v_lshl_add_u64 v[248:249], v[6:7], 0, 0
	v_lshl_add_u64 v[238:239], v[8:9], 0, 0
	global_load_dwordx4 v[190:193], v[6:7], off offset:256
	global_load_dwordx4 v[194:197], v[8:9], off offset:256
	global_load_dword v250, v[248:249], off offset:384
	global_load_dword v251, v[238:239], off offset:384
	s_waitcnt lgkmcnt(0)
	v_mfma_f32_16x16x32_bf16 v[152:155], v[172:175], v[186:189], v[152:155]
	s_waitcnt vmcnt(7)
	ds_write_b128 v75, v[178:181] offset:18432
	s_waitcnt vmcnt(6)
	ds_write_b128 v75, v[182:185] offset:27648
	s_waitcnt lgkmcnt(0)
	s_barrier
; #define LAS __attribute__((address_space(3)))
; __device__ __forceinline__ unsigned cvt_pk_bf16(float lo, float hi) { const float __attribute__((ext_vector_type(2))) v = {lo, hi}; return __builtin_bit_cast(unsigned, __builtin_convertvector(v, bf16x2_t)); }
; template <bool LOCAL>
; __device__ __forceinline__ void na_unit(const bf16* P, const bf16* VT, bf16* YCAT, const LAS float* rpb_l, LAS bf16* buf, int b, int gr, int hp, int qblk, int tid) {
;     ...
;             } else {
;                 const int cc = c - NLOC;
; #pragma unroll
;                 for (int p2 = 0; p2 < 2; ++p2) {
;                     float p[8];
; #pragma unroll
;                     for (int e = 0; e < 4; ++e) { p[e] = __expf(sc[4 * (cc >= 0 ? cc : 0) + 2 * p2][e] - m); p[4 + e] = __expf(sc[4 * (cc >= 0 ? cc : 0) + 2 * p2 + 1][e] - m); }
; #pragma unroll
;                     for (int e = 0; e < 8; ++e) lsum += p[e];
;                     const bf16x8 pf = __builtin_bit_cast(bf16x8, (v4u){pg8::cvt_pk_bf16(p[0], p[1]), pg8::cvt_pk_bf16(p[2], p[3]), pg8::cvt_pk_bf16(p[4], p[5]), pg8::cvt_pk_bf16(p[6], p[7])});
; #pragma unroll
;                     for (int dt = 0; dt < 4; ++dt) { const LAS bf16* vp = cb + (16 * dt + fr) * 72 + 32 * p2 + 4 * fq;
;                         o[dt] = __builtin_amdgcn_mfma_f32_16x16x32_bf16(frag44(vp, vp + 16), pf, o[dt], 0, 0, 0); }
;                 }
	v_fma_f32 v49, v49, s72, -v137
	ds_read2_b64 v[172:175], v52 offset1:4
	v_mul_f32_e32 v49, 0x3fb8aa3b, v49
	v_exp_f32_e32 v158, v49
	v_fma_f32 v49, v53, s72, -v137
	v_mul_f32_e32 v46, 0x3fb8aa3b, v46
	v_mul_f32_e32 v47, 0x3fb8aa3b, v47
	v_mul_f32_e32 v48, 0x3fb8aa3b, v48
	v_mul_f32_e32 v49, 0x3fb8aa3b, v49
	v_exp_f32_e32 v46, v46
	v_exp_f32_e32 v47, v47
	v_exp_f32_e32 v48, v48
	v_exp_f32_e32 v53, v49
	v_cvt_pk_bf16_f32 v176, v69, v50
	v_cvt_pk_bf16_f32 v177, v51, v158
	v_cvt_pk_bf16_f32 v178, v46, v47
	v_cvt_pk_bf16_f32 v179, v48, v53
	v_add_u32_e32 v180, 0x5000, v159
	v_add_u32_e32 v181, 0x5800, v159
	s_waitcnt lgkmcnt(0)
	v_mfma_f32_16x16x32_bf16 v[164:167], v[172:175], v[176:179], v[164:167]
	ds_read2_b64 v[172:175], v180 offset0:32 offset1:36
	v_add_u32_e32 v49, 0x6000, v159
	v_fma_f32 v38, v38, s72, -v137
	s_waitcnt lgkmcnt(0)
	v_mfma_f32_16x16x32_bf16 v[160:163], v[172:175], v[176:179], v[160:163]
	ds_read2_b64 v[172:175], v181 offset0:64 offset1:68
	v_mul_f32_e32 v38, 0x3fb8aa3b, v38
	v_fma_f32 v42, v42, s72, -v137
	s_waitcnt lgkmcnt(0)
	v_mfma_f32_16x16x32_bf16 v[168:171], v[172:175], v[176:179], v[168:171]
	ds_read2_b64 v[172:175], v49 offset0:96 offset1:100
	v_mul_f32_e32 v42, 0x3fb8aa3b, v42
	v_fma_f32 v30, v30, s72, -v137
	s_waitcnt lgkmcnt(0)
	v_mfma_f32_16x16x32_bf16 v[152:155], v[172:175], v[176:179], v[152:155]
	v_exp_f32_e32 v177, v38
	v_fma_f32 v38, v43, s72, -v137
	v_mul_f32_e32 v38, 0x3fb8aa3b, v38
	v_exp_f32_e32 v178, v38
	v_fma_f32 v38, v39, s72, -v137
	v_mul_f32_e32 v38, 0x3fb8aa3b, v38
	v_exp_f32_e32 v179, v38
	v_fma_f32 v38, v44, s72, -v137
	v_mul_f32_e32 v38, 0x3fb8aa3b, v38
	v_exp_f32_e32 v182, v38
	v_fma_f32 v38, v40, s72, -v137
	v_mul_f32_e32 v38, 0x3fb8aa3b, v38
	v_exp_f32_e32 v176, v42
	v_exp_f32_e32 v183, v38
	v_fma_f32 v38, v45, s72, -v137
	ds_read2_b64 v[42:45], v52 offset0:8 offset1:12
	v_mul_f32_e32 v38, 0x3fb8aa3b, v38
	v_exp_f32_e32 v184, v38
	v_fma_f32 v38, v41, s72, -v137
	v_mul_f32_e32 v38, 0x3fb8aa3b, v38
	v_exp_f32_e32 v185, v38
	v_cvt_pk_bf16_f32 v38, v176, v178
	v_cvt_pk_bf16_f32 v39, v182, v184
	v_cvt_pk_bf16_f32 v40, v177, v179
	v_cvt_pk_bf16_f32 v41, v183, v185
	v_mul_f32_e32 v30, 0x3fb8aa3b, v30
	v_fma_f32 v22, v22, s72, -v137
	s_waitcnt lgkmcnt(0)
	v_mfma_f32_16x16x32_bf16 v[42:45], v[42:45], v[38:41], v[164:167]
	v_mul_f32_e32 v22, 0x3fb8aa3b, v22
	v_fma_f32 v26, v26, s72, -v137
	v_mul_f32_e32 v26, 0x3fb8aa3b, v26
	ds_read2_b64 v[164:167], v180 offset0:40 offset1:44
	s_waitcnt lgkmcnt(0)
	v_mfma_f32_16x16x32_bf16 v[160:163], v[164:167], v[38:41], v[160:163]
	ds_read2_b64 v[164:167], v181 offset0:72 offset1:76
	v_fma_f32 v2, v2, s72, -v137
	v_mul_f32_e32 v2, 0x3fb8aa3b, v2
	s_waitcnt lgkmcnt(0)
	v_mfma_f32_16x16x32_bf16 v[164:167], v[164:167], v[38:41], v[168:171]
	s_nop 2
	ds_read2_b64 v[168:171], v49 offset0:104 offset1:108
	global_load_dwordx4 v[172:175], v[6:7], off offset:384
	s_nop 0
	global_load_dwordx4 v[6:9], v[8:9], off offset:384
	s_waitcnt vmcnt(5)
	ds_write_b128 v75, v[190:193]
	s_waitcnt vmcnt(4)
	ds_write_b128 v75, v[194:197] offset:9216
	s_waitcnt lgkmcnt(2)
	v_mfma_f32_16x16x32_bf16 v[38:41], v[168:171], v[38:41], v[152:155]
	v_exp_f32_e32 v168, v30
	v_fma_f32 v30, v34, s72, -v137
	v_mul_f32_e32 v30, 0x3fb8aa3b, v30
	v_exp_f32_e32 v169, v30
	v_fma_f32 v30, v31, s72, -v137
	v_mul_f32_e32 v30, 0x3fb8aa3b, v30
	v_exp_f32_e32 v170, v30
	v_fma_f32 v30, v35, s72, -v137
	v_mul_f32_e32 v30, 0x3fb8aa3b, v30
	v_exp_f32_e32 v171, v30
	v_fma_f32 v30, v32, s72, -v137
	v_mul_f32_e32 v30, 0x3fb8aa3b, v30
	v_exp_f32_e32 v186, v30
	v_fma_f32 v30, v36, s72, -v137
	v_mul_f32_e32 v30, 0x3fb8aa3b, v30
	v_exp_f32_e32 v187, v30
	v_fma_f32 v30, v33, s72, -v137
	s_waitcnt lgkmcnt(0)
	s_barrier
	v_mul_f32_e32 v34, 0x3fb8aa3b, v30
	ds_read2_b64 v[30:33], v159 offset1:4
	v_exp_f32_e32 v188, v34
	v_fma_f32 v34, v37, s72, -v137
	v_mul_f32_e32 v34, 0x3fb8aa3b, v34
	v_exp_f32_e32 v189, v34
	v_cvt_pk_bf16_f32 v34, v168, v170
	v_cvt_pk_bf16_f32 v35, v186, v188
	v_cvt_pk_bf16_f32 v36, v169, v171
	v_cvt_pk_bf16_f32 v37, v187, v189
	ds_read2_b64 v[152:155], v156 offset0:64 offset1:68
	v_fma_f32 v10, v10, s72, -v137
	s_waitcnt lgkmcnt(1)
	v_mfma_f32_16x16x32_bf16 v[30:33], v[30:33], v[34:37], v[42:45]
	v_mul_f32_e32 v10, 0x3fb8aa3b, v10
	s_nop 1
	ds_read2_b64 v[42:45], v151 offset0:32 offset1:36
	s_waitcnt lgkmcnt(0)
	v_mfma_f32_16x16x32_bf16 v[42:45], v[42:45], v[34:37], v[160:163]
	s_nop 2
	ds_read2_b64 v[160:163], v157 offset0:96 offset1:100
	v_mfma_f32_16x16x32_bf16 v[152:155], v[152:155], v[34:37], v[164:167]
	s_waitcnt lgkmcnt(0)
	v_mfma_f32_16x16x32_bf16 v[34:37], v[160:163], v[34:37], v[38:41]
	v_exp_f32_e32 v161, v22
	v_fma_f32 v22, v27, s72, -v137
	v_mul_f32_e32 v22, 0x3fb8aa3b, v22
	v_exp_f32_e32 v162, v22
	v_fma_f32 v22, v23, s72, -v137
	v_mul_f32_e32 v22, 0x3fb8aa3b, v22
	v_exp_f32_e32 v163, v22
	v_fma_f32 v22, v28, s72, -v137
	v_mul_f32_e32 v22, 0x3fb8aa3b, v22
	v_exp_f32_e32 v164, v22
	v_fma_f32 v22, v24, s72, -v137
	v_mul_f32_e32 v22, 0x3fb8aa3b, v22
	v_exp_f32_e32 v160, v26
	v_exp_f32_e32 v165, v22
	v_fma_f32 v22, v29, s72, -v137
	ds_read2_b64 v[26:29], v159 offset0:8 offset1:12
	v_mul_f32_e32 v22, 0x3fb8aa3b, v22
	v_exp_f32_e32 v159, v22
	v_fma_f32 v22, v25, s72, -v137
	v_mul_f32_e32 v22, 0x3fb8aa3b, v22
	v_exp_f32_e32 v166, v22
	v_cvt_pk_bf16_f32 v22, v160, v162
	v_cvt_pk_bf16_f32 v23, v164, v159
	v_cvt_pk_bf16_f32 v24, v161, v163
	v_cvt_pk_bf16_f32 v25, v165, v166
	ds_read2_b64 v[38:41], v156 offset0:72 offset1:76
	s_waitcnt lgkmcnt(1)
	v_mfma_f32_16x16x32_bf16 v[26:29], v[26:29], v[22:25], v[30:33]
	s_nop 2
	ds_read2_b64 v[30:33], v151 offset0:40 offset1:44
	s_waitcnt lgkmcnt(0)
	v_mfma_f32_16x16x32_bf16 v[30:33], v[30:33], v[22:25], v[42:45]
	s_nop 2
	ds_read2_b64 v[42:45], v157 offset0:104 offset1:108
	s_waitcnt vmcnt(1)
	ds_write_b128 v75, v[172:175] offset:18432
	s_waitcnt vmcnt(0)
	ds_write_b128 v75, v[6:9] offset:27648
	v_fma_f32 v6, v14, s72, -v137
	v_mul_f32_e32 v6, 0x3fb8aa3b, v6
	v_mfma_f32_16x16x32_bf16 v[38:41], v[38:41], v[22:25], v[152:155]
	s_waitcnt lgkmcnt(0)
	s_barrier
; #define LAS __attribute__((address_space(3)))
; __device__ __forceinline__ unsigned cvt_pk_bf16(float lo, float hi) { const float __attribute__((ext_vector_type(2))) v = {lo, hi}; return __builtin_bit_cast(unsigned, __builtin_convertvector(v, bf16x2_t)); }
; template <bool LOCAL>
; __device__ __forceinline__ void na_unit(const bf16* P, const bf16* VT, bf16* YCAT, const LAS float* rpb_l, LAS bf16* buf, int b, int gr, int hp, int qblk, int tid) {
;     ...
;             const int c = sidx - NCH;
;             if (LOCAL && c < 8) {
;                 float p[8];
; #pragma unroll
;                 for (int e = 0; e < 4; ++e) { p[e] = __expf(sl[2 * (c < 8 ? c : 0)][e] - m); p[4 + e] = __expf(sl[2 * (c < 8 ? c : 0) + 1][e] - m); }
; #pragma unroll
;                 for (int e = 0; e < 8; ++e) lsum += p[e];
;                 const bf16x8 pf = __builtin_bit_cast(bf16x8, (v4u){pg8::cvt_pk_bf16(p[0], p[1]), pg8::cvt_pk_bf16(p[2], p[3]), pg8::cvt_pk_bf16(p[4], p[5]), pg8::cvt_pk_bf16(p[6], p[7])});
; #pragma unroll
;                 for (int dt = 0; dt < 4; ++dt) { const LAS bf16* vp = cb + (16 * dt + fr) * 72 + kc0 + 4 * fq;
;                     o[dt] = __builtin_amdgcn_mfma_f32_16x16x32_bf16(frag44(vp, vp + 16), pf, o[dt], 0, 0, 0); }
;             } else {
;                 const int cc = c - NLOC;
; #pragma unroll
;                 for (int p2 = 0; p2 < 2; ++p2) {
;                     float p[8];
; #pragma unroll
;                     for (int e = 0; e < 4; ++e) { p[e] = __expf(sc[4 * (cc >= 0 ? cc : 0) + 2 * p2][e] - m); p[4 + e] = __expf(sc[4 * (cc >= 0 ? cc : 0) + 2 * p2 + 1][e] - m); }
; #pragma unroll
;                     for (int e = 0; e < 8; ++e) lsum += p[e];
;                     const bf16x8 pf = __builtin_bit_cast(bf16x8, (v4u){pg8::cvt_pk_bf16(p[0], p[1]), pg8::cvt_pk_bf16(p[2], p[3]), pg8::cvt_pk_bf16(p[4], p[5]), pg8::cvt_pk_bf16(p[6], p[7])});
; #pragma unroll
;                     for (int dt = 0; dt < 4; ++dt) { const LAS bf16* vp = cb + (16 * dt + fr) * 72 + 32 * p2 + 4 * fq;
;                         o[dt] = __builtin_amdgcn_mfma_f32_16x16x32_bf16(frag44(vp, vp + 16), pf, o[dt], 0, 0, 0); }
;                 }
;             }
;         }
;         if (sidx + 1 < 2 * NCH) NA_STORE(sidx + 1);
;         __syncthreads();
;     }
;     ...
;     lsum += __shfl_xor(lsum, 16); lsum += __shfl_xor(lsum, 32);
;     const float inv = 1.f / lsum;
	v_mfma_f32_16x16x32_bf16 v[22:25], v[42:45], v[22:25], v[34:37]
	v_ashrrev_i32_e32 v75, 31, v74
	s_nop 1
	v_exp_f32_e32 v34, v6
	v_fma_f32 v6, v18, s72, -v137
	v_mul_f32_e32 v6, 0x3fb8aa3b, v6
	v_exp_f32_e32 v35, v6
	v_fma_f32 v6, v15, s72, -v137
	v_mul_f32_e32 v6, 0x3fb8aa3b, v6
	v_exp_f32_e32 v36, v6
	v_fma_f32 v6, v19, s72, -v137
	v_mul_f32_e32 v6, 0x3fb8aa3b, v6
	v_exp_f32_e32 v37, v6
	v_fma_f32 v6, v16, s72, -v137
	v_mul_f32_e32 v6, 0x3fb8aa3b, v6
	v_exp_f32_e32 v42, v6
	v_fma_f32 v6, v20, s72, -v137
	v_mul_f32_e32 v6, 0x3fb8aa3b, v6
	v_exp_f32_e32 v43, v6
	v_fma_f32 v6, v17, s72, -v137
	v_mul_f32_e32 v14, 0x3fb8aa3b, v6
	ds_read2_b64 v[6:9], v52 offset1:4
	v_exp_f32_e32 v44, v14
	v_fma_f32 v14, v21, s72, -v137
	v_mul_f32_e32 v14, 0x3fb8aa3b, v14
	v_exp_f32_e32 v45, v14
	v_cvt_pk_bf16_f32 v14, v34, v36
	v_cvt_pk_bf16_f32 v15, v42, v44
	v_cvt_pk_bf16_f32 v16, v35, v37
	v_cvt_pk_bf16_f32 v17, v43, v45
	ds_read2_b64 v[18:21], v180 offset0:32 offset1:36
	s_waitcnt lgkmcnt(1)
	v_mfma_f32_16x16x32_bf16 v[6:9], v[6:9], v[14:17], v[26:29]
	s_nop 2
	ds_read2_b64 v[26:29], v181 offset0:64 offset1:68
	s_waitcnt lgkmcnt(0)
	v_mfma_f32_16x16x32_bf16 v[26:29], v[26:29], v[14:17], v[38:41]
	s_nop 2
	v_add_f32_e32 v38, 0, v133
	v_add_f32_e32 v38, v97, v38
	v_add_f32_e32 v38, v96, v38
	v_add_f32_e32 v38, v100, v38
	v_add_f32_e32 v38, v93, v38
	v_add_f32_e32 v38, v92, v38
	v_add_f32_e32 v38, v95, v38
	v_add_f32_e32 v38, v94, v38
	v_add_f32_e32 v38, v87, v38
	v_add_f32_e32 v38, v91, v38
	v_add_f32_e32 v38, v99, v38
	v_add_f32_e32 v38, v101, v38
	v_add_f32_e32 v38, v76, v38
	v_add_f32_e32 v38, v88, v38
	v_add_f32_e32 v38, v98, v38
	v_add_f32_e32 v38, v102, v38
	v_add_f32_e32 v38, v104, v38
	v_add_f32_e32 v38, v106, v38
	v_add_f32_e32 v38, v108, v38
	v_add_f32_e32 v38, v109, v38
	v_add_f32_e32 v38, v103, v38
	v_add_f32_e32 v38, v105, v38
	v_add_f32_e32 v38, v107, v38
	v_add_f32_e32 v38, v110, v38
	v_add_f32_e32 v38, v112, v38
	v_add_f32_e32 v38, v114, v38
	v_add_f32_e32 v38, v116, v38
	v_add_f32_e32 v38, v117, v38
	v_add_f32_e32 v38, v111, v38
	v_add_f32_e32 v38, v113, v38
	v_add_f32_e32 v38, v115, v38
	v_add_f32_e32 v38, v118, v38
	v_add_f32_e32 v38, v120, v38
	v_add_f32_e32 v38, v122, v38
	v_add_f32_e32 v38, v124, v38
	v_add_f32_e32 v38, v125, v38
	v_add_f32_e32 v38, v119, v38
	v_add_f32_e32 v38, v121, v38
	v_add_f32_e32 v38, v123, v38
	v_add_f32_e32 v38, v126, v38
	v_add_f32_e32 v38, v128, v38
	v_add_f32_e32 v38, v130, v38
	v_add_f32_e32 v38, v132, v38
	v_add_f32_e32 v38, v134, v38
	v_add_f32_e32 v38, v127, v38
	v_add_f32_e32 v38, v129, v38
	v_add_f32_e32 v38, v131, v38
	v_add_f32_e32 v38, v135, v38
	v_add_f32_e32 v38, v138, v38
	v_add_f32_e32 v38, v140, v38
	v_add_f32_e32 v38, v142, v38
	v_add_f32_e32 v38, v143, v38
	v_add_f32_e32 v38, v136, v38
	v_add_f32_e32 v38, v139, v38
	v_add_f32_e32 v38, v141, v38
	v_add_f32_e32 v38, v144, v38
	v_add_f32_e32 v38, v78, v38
	v_add_f32_e32 v38, v80, v38
	v_add_f32_e32 v38, v145, v38
	v_add_f32_e32 v38, v149, v38
	v_add_f32_e32 v38, v70, v38
	v_add_f32_e32 v38, v79, v38
	v_add_f32_e32 v38, v81, v38
	v_add_f32_e32 v38, v148, v38
	v_add_f32_e32 v38, v150, v38
	v_add_f32_e32 v38, v66, v38
	v_add_f32_e32 v38, v67, v38
	v_add_f32_e32 v38, v68, v38
	v_add_f32_e32 v38, v62, v38
	v_add_f32_e32 v38, v63, v38
	v_add_f32_e32 v38, v64, v38
	v_add_f32_e32 v38, v65, v38
	v_add_f32_e32 v38, v58, v38
	v_add_f32_e32 v38, v59, v38
	v_add_f32_e32 v38, v60, v38
	v_add_f32_e32 v38, v61, v38
	v_add_f32_e32 v38, v54, v38
	v_add_f32_e32 v38, v55, v38
	v_add_f32_e32 v38, v56, v38
	v_add_f32_e32 v38, v57, v38
	v_add_f32_e32 v38, v69, v38
	v_add_f32_e32 v38, v50, v38
	v_add_f32_e32 v38, v51, v38
	v_add_f32_e32 v38, v158, v38
	v_add_f32_e32 v38, v46, v38
	v_add_f32_e32 v38, v47, v38
	v_add_f32_e32 v38, v48, v38
	v_add_f32_e32 v38, v53, v38
	v_add_f32_e32 v38, v176, v38
	v_mfma_f32_16x16x32_bf16 v[18:21], v[18:21], v[14:17], v[30:33]
	v_add_f32_e32 v38, v178, v38
	v_add_f32_e32 v38, v182, v38
	v_add_f32_e32 v38, v184, v38
	ds_read2_b64 v[30:33], v49 offset0:96 offset1:100
	v_add_f32_e32 v38, v177, v38
	v_add_f32_e32 v38, v179, v38
	v_add_f32_e32 v38, v183, v38
	v_add_f32_e32 v38, v185, v38
	v_add_f32_e32 v38, v168, v38
	v_add_f32_e32 v38, v170, v38
	s_waitcnt lgkmcnt(0)
	v_mfma_f32_16x16x32_bf16 v[14:17], v[30:33], v[14:17], v[22:25]
	v_add_f32_e32 v38, v186, v38
	s_nop 1
	v_exp_f32_e32 v23, v2
	v_fma_f32 v2, v11, s72, -v137
	v_mul_f32_e32 v2, 0x3fb8aa3b, v2
	v_add_f32_e32 v38, v188, v38
	v_exp_f32_e32 v24, v2
	v_fma_f32 v2, v3, s72, -v137
	v_add_f32_e32 v38, v169, v38
	v_mul_f32_e32 v2, 0x3fb8aa3b, v2
	v_add_f32_e32 v38, v171, v38
	v_exp_f32_e32 v25, v2
	v_fma_f32 v2, v12, s72, -v137
	v_add_f32_e32 v38, v187, v38
	v_mul_f32_e32 v2, 0x3fb8aa3b, v2
	v_add_f32_e32 v38, v189, v38
	v_exp_f32_e32 v30, v2
	v_fma_f32 v2, v4, s72, -v137
	v_add_f32_e32 v38, v160, v38
	v_mul_f32_e32 v2, 0x3fb8aa3b, v2
	v_add_f32_e32 v38, v162, v38
	v_exp_f32_e32 v22, v10
	v_exp_f32_e32 v31, v2
	v_fma_f32 v2, v13, s72, -v137
	ds_read2_b64 v[10:13], v52 offset0:8 offset1:12
	v_add_f32_e32 v38, v164, v38
	v_mul_f32_e32 v2, 0x3fb8aa3b, v2
	v_add_f32_e32 v38, v159, v38
	v_exp_f32_e32 v32, v2
	v_fma_f32 v2, v5, s72, -v137
	v_add_f32_e32 v38, v161, v38
	v_mul_f32_e32 v2, 0x3fb8aa3b, v2
	v_add_f32_e32 v38, v163, v38
	v_exp_f32_e32 v33, v2
	v_add_f32_e32 v38, v165, v38
	v_add_f32_e32 v38, v166, v38
	v_add_f32_e32 v34, v34, v38
	v_add_f32_e32 v34, v36, v34
	v_cvt_pk_bf16_f32 v2, v22, v24
	v_cvt_pk_bf16_f32 v3, v30, v32
	v_cvt_pk_bf16_f32 v4, v23, v25
	v_cvt_pk_bf16_f32 v5, v31, v33
	v_add_f32_e32 v34, v42, v34
	v_add_f32_e32 v34, v44, v34
	s_waitcnt lgkmcnt(0)
	v_mfma_f32_16x16x32_bf16 v[6:9], v[10:13], v[2:5], v[6:9]
	ds_read2_b64 v[10:13], v180 offset0:40 offset1:44
	v_add_f32_e32 v34, v35, v34
	v_add_f32_e32 v34, v37, v34
	v_add_f32_e32 v34, v43, v34
	v_add_f32_e32 v34, v45, v34
	v_add_f32_e32 v22, v22, v34
	v_add_f32_e32 v22, v24, v22
	v_add_f32_e32 v22, v30, v22
	v_add_f32_e32 v22, v32, v22
	s_waitcnt lgkmcnt(0)
	v_mfma_f32_16x16x32_bf16 v[10:13], v[10:13], v[2:5], v[18:21]
	v_add_f32_e32 v22, v23, v22
	v_add_f32_e32 v22, v25, v22
	v_add_f32_e32 v22, v31, v22
	ds_read2_b64 v[18:21], v181 offset0:72 offset1:76
	v_add_f32_e32 v30, v33, v22
	ds_bpermute_b32 v31, v89, v30
	ds_read2_b64 v[22:25], v49 offset0:104 offset1:108
	s_waitcnt lgkmcnt(2)
	v_mfma_f32_16x16x32_bf16 v[18:21], v[18:21], v[2:5], v[26:29]
	s_waitcnt lgkmcnt(1)
	s_nop 1
	v_add_f32_e32 v26, v30, v31
	ds_bpermute_b32 v27, v90, v26
	v_lshlrev_b32_e32 v70, 1, v77
	s_waitcnt lgkmcnt(1)
	v_mfma_f32_16x16x32_bf16 v[14:17], v[22:25], v[2:5], v[14:17]
	s_waitcnt lgkmcnt(0)
	s_barrier
; __device__ __forceinline__ unsigned cvt_pk_bf16(float lo, float hi) { const float __attribute__((ext_vector_type(2))) v = {lo, hi}; return __builtin_bit_cast(unsigned, __builtin_convertvector(v, bf16x2_t)); }
; template <bool LOCAL>
; __device__ __forceinline__ void na_unit(const bf16* P, const bf16* VT, bf16* YCAT, const LAS float* rpb_l, LAS bf16* buf, int b, int gr, int hp, int qblk, int tid) {
;     ...
;     lsum += __shfl_xor(lsum, 16); lsum += __shfl_xor(lsum, 32);
;     const float inv = 1.f / lsum;
;     bf16* op = YCAT + (size_t)(qrow0 + fr) * D + 512 + h * 64 + 4 * fq;
; #pragma unroll
;     for (int dt = 0; dt < 4; ++dt) { v2u w; w.x = pg8::cvt_pk_bf16(o[dt][0] * inv, o[dt][1] * inv); w.y = pg8::cvt_pk_bf16(o[dt][2] * inv, o[dt][3] * inv); *(v2u*)(op + dt * 16) = w; }
	v_add_f32_e32 v2, v26, v27
	v_div_scale_f32 v3, s[0:1], v2, v2, 1.0
	v_rcp_f32_e32 v4, v3
	s_nop 0
	v_fma_f32 v5, -v3, v4, 1.0
	v_fmac_f32_e32 v4, v5, v4
	v_div_scale_f32 v5, vcc, 1.0, v2, 1.0
	v_mul_f32_e32 v22, v5, v4
	v_fma_f32 v23, -v3, v22, v5
	v_fmac_f32_e32 v22, v23, v4
	v_fma_f32 v3, -v3, v22, v5
	v_div_fmas_f32 v3, v3, v4, v22
	v_div_fixup_f32 v22, v3, v2, 1.0
	v_lshlrev_b64 v[2:3], 11, v[74:75]
	v_lshl_add_u64 v[2:3], s[10:11], 0, v[2:3]
	v_lshl_add_u64 v[2:3], v[72:73], 1, v[2:3]
	v_pk_mul_f32 v[6:7], v[6:7], v[22:23] op_sel_hi:[1,0]
	v_pk_mul_f32 v[8:9], v[8:9], v[22:23] op_sel_hi:[1,0]
	v_lshl_add_u64 v[4:5], v[2:3], 0, v[70:71]
	v_cvt_pk_bf16_f32 v6, v6, v7
	v_cvt_pk_bf16_f32 v7, v8, v9
	global_store_dwordx2 v[4:5], v[6:7], off offset:1024
	v_pk_mul_f32 v[6:7], v[10:11], v[22:23] op_sel_hi:[1,0]
	v_pk_mul_f32 v[8:9], v[12:13], v[22:23] op_sel_hi:[1,0]
	v_cvt_pk_bf16_f32 v6, v6, v7
	v_cvt_pk_bf16_f32 v7, v8, v9
	global_store_dwordx2 v[4:5], v[6:7], off offset:1056
	v_pk_mul_f32 v[6:7], v[18:19], v[22:23] op_sel_hi:[1,0]
	v_pk_mul_f32 v[8:9], v[20:21], v[22:23] op_sel_hi:[1,0]
	v_cvt_pk_bf16_f32 v6, v6, v7
	v_cvt_pk_bf16_f32 v7, v8, v9
	v_lshl_add_u64 v[2:3], v[4:5], 0, s[12:13]
	global_store_dwordx2 v[4:5], v[6:7], off offset:1088
	v_pk_mul_f32 v[4:5], v[14:15], v[22:23] op_sel_hi:[1,0]
	v_pk_mul_f32 v[6:7], v[16:17], v[22:23] op_sel_hi:[1,0]
	v_cvt_pk_bf16_f32 v4, v4, v5

; #define LAS __attribute__((address_space(3)))
; template <bool LOCAL>
; __device__ __forceinline__ void na_unit(const bf16* P, const bf16* VT, bf16* YCAT, const LAS float* rpb_l, LAS bf16* buf, int b, int gr, int hp, int qblk, int tid) {
;     typedef pg8::bf16x8 bf16x8;
;     constexpr int NCH = LOCAL ? 12 : 4, NLOC = LOCAL ? 8 : 0;
;     const int lane = tid & 63, wv = tid >> 6, fr = lane & 15, fq = lane >> 4, hh = wv >> 2, qb = wv & 3, h = 2 * hp + hh;
;     const int qrow0 = LOCAL ? NCTX + b * SEQ + gr * 64 + 16 * qb : b * CTXL + qblk * 64 + 16 * qb;
;     const int r0 = min(max(gr - 4, 0), 24);
;     const int kc0 = qb == 0 ? 0 : qb == 1 ? 8 : qb == 2 ? 24 : 32;
;     const int qcol = 16 * qb + fr, cs = min(max(qcol - 8, 0), 48);
;     const LAS float* rpb = rpb_l + h * 15 * 31;
;     v4u ld[2][2];
;     const int lrow = (tid >> 3) & 63, lseg = tid & 7;
;     ...
;     bf16x8 qf[2];
; #pragma unroll
;     for (int ks = 0; ks < 2; ++ks) qf[ks] = *(const bf16x8*)(P + (size_t)(qrow0 + fr) * DINP + h * 64 + 32 * ks + 8 * fq);
;     f32x4 sl[16], sc[16];
;     float m = -1.0e30f, lsum = 0.f;
;     f32x4 o[4];
; #pragma unroll
;     for (int dt = 0; dt < 4; ++dt) o[dt] = (f32x4){0.f, 0.f, 0.f, 0.f};
;     NA_ISSUE(0); NA_ISSUE(1); NA_STORE(0);
;     __syncthreads();
; #pragma unroll
;     for (int sidx = 0; sidx < 2 * NCH; ++sidx) {
;         if (sidx + 2 < 2 * NCH) NA_ISSUE(sidx + 2);
;         const LAS bf16* cb = buf + (sidx & 1) * 9216 + hh * 4608;
;         if (sidx < NCH) {
;             const int c = sidx;
;             if (LOCAL && c < 8) {
; #pragma unroll
;                 for (int t2 = 0; t2 < 2; ++t2) {
;                     const LAS bf16* kp = cb + (kc0 + 16 * t2 + fr) * 72 + 8 * fq;
;                     f32x4 acc = {0.f, 0.f, 0.f, 0.f};
;                     acc = __builtin_amdgcn_mfma_f32_16x16x32_bf16(*(const LAS bf16x8*)(kp), qf[0], acc, 0, 0, 0);
;                     acc = __builtin_amdgcn_mfma_f32_16x16x32_bf16(*(const LAS bf16x8*)(kp + 32), qf[1], acc, 0, 0, 0);
;                     const LAS float* rb = rpb + (r0 + c - gr + 7) * 31 + 15 - qcol;
; #pragma unroll
;                     for (int e = 0; e < 4; ++e) { const int kcol = kc0 + 16 * t2 + 4 * fq + e; const bool ok = (kcol >= cs) && (kcol < cs + 16);
;                         const float sv = ok ? acc[e] * 0.125f + rb[ok ? kcol : qcol] : -1.0e30f; acc[e] = sv; m = fmaxf(m, sv); }
.LBB0_636:
	v_mov_b32_e32 v93, v0
	s_movk_i32 s2, 0x2400
	v_and_b32_e32 v89, 15, v93
	v_bfe_u32 v91, v93, 4, 2
	v_ashrrev_i32_e32 v92, 8, v93
	s_mov_b64 s[0:1], -1
	s_cmpk_gt_i32 s76, 0x7ff
	v_bfe_u32 v88, v93, 3, 6
	v_lshlrev_b32_e32 v76, 3, v91
	v_lshlrev_b32_e32 v70, 4, v91
	v_mad_i32_i24 v86, v92, s2, 0
	v_mul_u32_u24_e32 v87, 0x90, v89
	s_waitcnt lgkmcnt(0)
	s_barrier
	s_cbranch_scc0 .LBB0_638
	s_lshl_b32 s0, s76, 4
	s_and_b32 s0, s0, 0xffffff00
	s_addk_i32 s0, 0x8000
	v_mov_b64_e32 v[78:79], s[8:9]
	s_lshl_b32 s1, s76, 5
	v_or_b32_e32 v77, s0, v88
	v_lshlrev_b32_e32 v4, 4, v93
	s_and_b32 s16, s1, 0x180
	v_mad_u64_u32 v[2:3], s[14:15], v77, s70, v[78:79]
	v_and_b32_e32 v80, 0x70, v4
	v_mov_b32_e32 v81, v71
	v_lshl_add_u64 v[2:3], v[2:3], 0, v[80:81]
	s_lshl_b32 s2, s16, 1
	v_lshl_add_u64 v[2:3], v[2:3], 0, s[2:3]
	global_load_dwordx4 v[6:9], v[2:3], off offset:1024
	global_load_dwordx4 v[10:13], v[2:3], off offset:1152
	s_lshl_b32 s1, s76, 6
	s_and_b32 s1, s1, 0xc0
	v_lshrrev_b32_e32 v2, 2, v93
	v_and_or_b32 v2, v2, 48, s1
	v_lshl_add_u32 v4, v92, 6, s16
	v_or3_b32 v72, v2, v89, s0
	v_ashrrev_i32_e32 v5, 31, v4
	v_mad_u64_u32 v[2:3], s[14:15], v72, s70, v[78:79]
	v_lshlrev_b64 v[74:75], 1, v[4:5]
	v_lshl_add_u64 v[2:3], v[2:3], 0, v[74:75]
	v_or_b32_e32 v14, 64, v77
	v_lshl_add_u64 v[22:23], v[2:3], 0, v[70:71]
	v_mad_u64_u32 v[14:15], s[14:15], v14, s70, v[78:79]
	global_load_dwordx4 v[2:5], v[22:23], off
	v_lshl_add_u64 v[14:15], v[14:15], 0, v[80:81]
	v_lshl_add_u64 v[18:19], v[14:15], 0, s[2:3]
	s_mov_b32 s100, 0x60000
	s_mov_b32 s101, 0
	v_lshl_add_u64 v[248:249], v[18:19], 0, s[100:101]
	global_load_dwordx4 v[14:17], v[18:19], off offset:1024
	s_nop 0
	global_load_dwordx4 v[18:21], v[18:19], off offset:1152
	global_load_dword v250, v[248:249], off offset:1024
	global_load_dword v251, v[248:249], off offset:1152
	s_nop 0
	global_load_dwordx4 v[50:53], v[22:23], off offset:64
	v_mul_u32_u24_e32 v22, 0x90, v88
	v_add3_u32 v73, 0, v22, v80
	v_or_b32_e32 v22, 0x80, v77
	v_add3_u32 v90, v86, v70, v87
	s_mov_b32 s1, s3
	v_cmp_lt_i32_e32 vcc, v83, v84
	s_waitcnt vmcnt(7)
	ds_write_b128 v73, v[6:9]
	s_waitcnt vmcnt(6)
	ds_write_b128 v73, v[10:13] offset:9216
	v_mad_u64_u32 v[10:11], s[14:15], v22, s70, v[78:79]
	v_lshl_add_u64 v[10:11], v[10:11], 0, v[80:81]
	v_lshl_add_u64 v[26:27], v[10:11], 0, s[2:3]
	s_waitcnt lgkmcnt(0)
	s_barrier
	ds_read_b128 v[6:9], v90
	ds_read_b128 v[10:13], v90 offset:2304
	v_lshl_add_u64 v[248:249], v[26:27], 0, s[100:101]
	global_load_dwordx4 v[22:25], v[26:27], off offset:1024
	global_load_dwordx4 v[30:33], v[26:27], off offset:1152
	global_load_dword v250, v[248:249], off offset:1024
	global_load_dword v251, v[248:249], off offset:1152
	ds_read_b128 v[26:29], v90 offset:64
	ds_read_b128 v[34:37], v90 offset:4608
	ds_read_b128 v[38:41], v90 offset:2368
	ds_read_b128 v[42:45], v90 offset:4672
	ds_read_b128 v[46:49], v90 offset:6912
	s_waitcnt vmcnt(9) lgkmcnt(6)
	v_mfma_f32_16x16x32_bf16 v[6:9], v[6:9], v[2:5], 0
	ds_read_b128 v[54:57], v90 offset:6976
	s_waitcnt vmcnt(8)
	ds_write_b128 v73, v[14:17] offset:18432
	s_waitcnt vmcnt(7)
	ds_write_b128 v73, v[18:21] offset:27648
	s_waitcnt lgkmcnt(0)
	v_mfma_f32_16x16x32_bf16 v[10:13], v[10:13], v[2:5], 0
	s_barrier
	v_mfma_f32_16x16x32_bf16 v[14:17], v[34:37], v[2:5], 0
	v_mfma_f32_16x16x32_bf16 v[18:21], v[46:49], v[2:5], 0
	ds_read_b128 v[34:37], v90 offset:18432
	ds_read_b128 v[46:49], v90 offset:18496
	ds_read_b128 v[58:61], v90 offset:20736
	ds_read_b128 v[94:97], v90 offset:20800
	s_waitcnt vmcnt(4)
	v_mfma_f32_16x16x32_bf16 v[62:65], v[26:29], v[50:53], v[6:9]
	s_nop 2
	v_or_b32_e32 v6, s16, v88
	s_waitcnt lgkmcnt(1)
	v_mfma_f32_16x16x32_bf16 v[98:101], v[58:61], v[2:5], 0
	ds_read_b128 v[58:61], v90 offset:23040
	ds_read_b128 v[102:105], v90 offset:23104
	v_mul_u32_u24_e32 v8, 0x9000, v6
	v_mov_b32_e32 v7, v71
	v_mfma_f32_16x16x32_bf16 v[66:69], v[38:41], v[50:53], v[10:13]
	v_mov_b32_e32 v9, v71
	s_nop 1
	v_lshl_add_u64 v[10:11], s[4:5], 0, v[80:81]
	v_or_b32_e32 v12, 64, v6
	v_or_b32_e32 v13, 0xc0, v77
	v_lshl_add_u64 v[10:11], s[0:1], 1, v[10:11]
	v_lshlrev_b32_e32 v6, 1, v8
	v_mul_u32_u24_e32 v8, 0x9000, v12
	v_mad_u64_u32 v[12:13], s[0:1], v13, s70, v[78:79]
	v_lshl_add_u64 v[78:79], v[10:11], 0, v[6:7]
	v_lshlrev_b32_e32 v8, 1, v8
	v_lshl_add_u64 v[6:7], v[12:13], 0, v[80:81]
	v_lshl_add_u64 v[80:81], v[10:11], 0, v[8:9]
	v_lshl_add_u64 v[10:11], v[6:7], 0, s[2:3]
	s_waitcnt lgkmcnt(1)
	v_mfma_f32_16x16x32_bf16 v[106:109], v[58:61], v[2:5], 0
	ds_read_b128 v[58:61], v90 offset:25344
	ds_read_b128 v[110:113], v90 offset:25408
	global_load_dwordx4 v[6:9], v[10:11], off offset:1024
	s_nop 0
	global_load_dwordx4 v[10:13], v[10:11], off offset:1152
	v_mul_f32_e32 v38, 0x3e000000, v68
	s_waitcnt lgkmcnt(1)
	v_mfma_f32_16x16x32_bf16 v[114:117], v[58:61], v[2:5], 0
	v_mul_f32_e32 v39, 0x3e000000, v69
	s_waitcnt vmcnt(5)
	ds_write_b128 v73, v[22:25]
	s_waitcnt vmcnt(4)
	ds_write_b128 v73, v[30:33] offset:9216
	v_mfma_f32_16x16x32_bf16 v[58:61], v[42:45], v[50:53], v[14:17]
	s_waitcnt lgkmcnt(0)
	s_barrier
; #define LAS __attribute__((address_space(3)))
; template <bool LOCAL>
; __device__ __forceinline__ void na_unit(const bf16* P, const bf16* VT, bf16* YCAT, const LAS float* rpb_l, LAS bf16* buf, int b, int gr, int hp, int qblk, int tid) {
;     ...
;     for (int sidx = 0; sidx < 2 * NCH; ++sidx) {
;         if (sidx + 2 < 2 * NCH) NA_ISSUE(sidx + 2);
;         const LAS bf16* cb = buf + (sidx & 1) * 9216 + hh * 4608;
;         if (sidx < NCH) {
;             const int c = sidx;
;             if (LOCAL && c < 8) {
; #pragma unroll
;                 for (int t2 = 0; t2 < 2; ++t2) {
;                     const LAS bf16* kp = cb + (kc0 + 16 * t2 + fr) * 72 + 8 * fq;
;                     f32x4 acc = {0.f, 0.f, 0.f, 0.f};
;                     acc = __builtin_amdgcn_mfma_f32_16x16x32_bf16(*(const LAS bf16x8*)(kp), qf[0], acc, 0, 0, 0);
;                     acc = __builtin_amdgcn_mfma_f32_16x16x32_bf16(*(const LAS bf16x8*)(kp + 32), qf[1], acc, 0, 0, 0);
;                     const LAS float* rb = rpb + (r0 + c - gr + 7) * 31 + 15 - qcol;
; #pragma unroll
;                     for (int e = 0; e < 4; ++e) { const int kcol = kc0 + 16 * t2 + 4 * fq + e; const bool ok = (kcol >= cs) && (kcol < cs + 16);
;                         const float sv = ok ? acc[e] * 0.125f + rb[ok ? kcol : qcol] : -1.0e30f; acc[e] = sv; m = fmaxf(m, sv); }
;                     sl[2 * (c < 8 ? c : 0) + t2] = acc; }
;             } else {
;                 const int cc = c - NLOC;
; #pragma unroll
;                 for (int t4 = 0; t4 < 4; ++t4) {
;                     const LAS bf16* kp = cb + (16 * t4 + fr) * 72 + 8 * fq;
;                     f32x4 acc = {0.f, 0.f, 0.f, 0.f};
;                     acc = __builtin_amdgcn_mfma_f32_16x16x32_bf16(*(const LAS bf16x8*)(kp), qf[0], acc, 0, 0, 0);
;                     acc = __builtin_amdgcn_mfma_f32_16x16x32_bf16(*(const LAS bf16x8*)(kp + 32), qf[1], acc, 0, 0, 0);
; #pragma unroll
;                     for (int e = 0; e < 4; ++e) { acc[e] *= 0.125f; m = fmaxf(m, acc[e]); }
;                     sc[4 * (cc >= 0 ? cc : 0) + t4] = acc; }
;             }
;             if (sidx == NCH - 1) { m = fmaxf(m, __shfl_xor(m, 16)); m = fmaxf(m, __shfl_xor(m, 32)); }
	s_nop 0
	v_mul_f32_e32 v14, 0x3e000000, v62
	v_mul_f32_e32 v15, 0x3e000000, v63
	v_mfma_f32_16x16x32_bf16 v[54:57], v[54:57], v[50:53], v[18:21]
	s_nop 1
	v_mul_f32_e32 v40, 0x3e000000, v58
	v_mul_f32_e32 v41, 0x3e000000, v59
	v_mul_f32_e32 v77, 0x3e000000, v60
	v_mfma_f32_16x16x32_bf16 v[42:45], v[94:97], v[50:53], v[98:101]
	v_mul_f32_e32 v18, 0x3e000000, v64
	v_mul_f32_e32 v19, 0x3e000000, v65
	v_mul_f32_e32 v20, 0x3e000000, v66
	v_max3_f32 v99, v14, s73, v15
	v_mul_f32_e32 v21, 0x3e000000, v67
	v_max3_f32 v18, v99, v18, v19
	v_mfma_f32_16x16x32_bf16 v[34:37], v[34:37], v[2:5], 0
	v_max3_f32 v18, v18, v20, v21
	ds_read_b128 v[14:17], v90
	v_max3_f32 v22, v18, v38, v39
	ds_read_b128 v[18:21], v90 offset:2304
	v_mul_f32_e32 v94, 0x3e000000, v61
	v_max3_f32 v22, v22, v40, v41
	v_mul_f32_e32 v95, 0x3e000000, v54
	v_mul_f32_e32 v96, 0x3e000000, v55
	v_max3_f32 v38, v22, v77, v94
	v_mfma_f32_16x16x32_bf16 v[46:49], v[46:49], v[50:53], v[34:37]
	v_mul_f32_e32 v97, 0x3e000000, v56
	v_mul_f32_e32 v98, 0x3e000000, v57
	v_max3_f32 v38, v38, v95, v96
	ds_read_b128 v[22:25], v90 offset:64
	ds_read_b128 v[30:33], v90 offset:4608
	v_max3_f32 v38, v38, v97, v98
	ds_read_b128 v[94:97], v90 offset:2368
	v_mfma_f32_16x16x32_bf16 v[34:37], v[102:105], v[50:53], v[106:109]
	v_mul_f32_e32 v100, 0x3e000000, v46
	v_mul_f32_e32 v101, 0x3e000000, v47
	v_mul_f32_e32 v102, 0x3e000000, v48
	v_mul_f32_e32 v103, 0x3e000000, v49
	v_max3_f32 v38, v38, v100, v101
	v_mul_f32_e32 v106, 0x3e000000, v42
	v_mul_f32_e32 v107, 0x3e000000, v43
	s_waitcnt lgkmcnt(4)
	v_mfma_f32_16x16x32_bf16 v[14:17], v[14:17], v[2:5], 0
	v_max3_f32 v38, v38, v102, v103
	v_mul_f32_e32 v108, 0x3e000000, v44
	v_mul_f32_e32 v109, 0x3e000000, v45
	s_waitcnt lgkmcnt(3)
	v_mfma_f32_16x16x32_bf16 v[18:21], v[18:21], v[2:5], 0
	ds_read_b128 v[98:101], v90 offset:4672
	s_waitcnt lgkmcnt(2)
	v_mfma_f32_16x16x32_bf16 v[102:105], v[30:33], v[2:5], 0
	v_max3_f32 v30, v38, v106, v107
	v_max3_f32 v30, v30, v108, v109
	v_mfma_f32_16x16x32_bf16 v[26:29], v[110:113], v[50:53], v[114:117]
	v_mul_f32_e32 v110, 0x3e000000, v34
	v_mul_f32_e32 v111, 0x3e000000, v35
	v_mul_f32_e32 v112, 0x3e000000, v36
	v_mul_f32_e32 v113, 0x3e000000, v37
	v_max3_f32 v30, v30, v110, v111
	v_mfma_f32_16x16x32_bf16 v[38:41], v[22:25], v[50:53], v[14:17]
	s_nop 1
	v_mul_f32_e32 v114, 0x3e000000, v26
	v_mul_f32_e32 v115, 0x3e000000, v27
	v_mul_f32_e32 v116, 0x3e000000, v28
	v_max3_f32 v14, v30, v112, v113
	s_waitcnt lgkmcnt(1)
	v_mfma_f32_16x16x32_bf16 v[30:33], v[94:97], v[50:53], v[18:21]
	v_lshl_add_u64 v[248:249], v[78:79], 0, 0
	v_lshl_add_u64 v[238:239], v[80:81], 0, 0
	global_load_dwordx4 v[94:97], v[78:79], off
	global_load_dwordx4 v[106:109], v[80:81], off
	global_load_dword v250, v[248:249], off offset:128
	global_load_dword v251, v[238:239], off offset:128
	v_mul_f32_e32 v117, 0x3e000000, v29
	v_max3_f32 v14, v14, v114, v115
	v_max3_f32 v22, v14, v116, v117
	ds_read_b128 v[14:17], v90 offset:6912
	v_mul_f32_e32 v23, 0x3e000000, v38
	v_mul_f32_e32 v24, 0x3e000000, v39
	v_mul_f32_e32 v25, 0x3e000000, v40
	v_mul_f32_e32 v77, 0x3e000000, v41
	v_max3_f32 v22, v22, v23, v24
	s_waitcnt lgkmcnt(1)
	v_mfma_f32_16x16x32_bf16 v[18:21], v[98:101], v[50:53], v[102:105]
	v_mul_f32_e32 v98, 0x3e000000, v30
	v_mul_f32_e32 v99, 0x3e000000, v31
	v_max3_f32 v22, v22, v25, v77
	v_max3_f32 v77, v22, v98, v99
	ds_read_b128 v[22:25], v90 offset:6976
	s_waitcnt vmcnt(5)
	ds_write_b128 v73, v[6:9] offset:18432
	s_waitcnt vmcnt(4)
	ds_write_b128 v73, v[10:13] offset:27648
	s_waitcnt lgkmcnt(0)
	s_barrier
	ds_read_b128 v[6:9], v90 offset:18432
	v_mul_f32_e32 v100, 0x3e000000, v32
	v_mul_f32_e32 v10, 0x3e000000, v33
	v_mfma_f32_16x16x32_bf16 v[14:17], v[14:17], v[2:5], 0
	v_max3_f32 v77, v77, v100, v10
	ds_read_b128 v[10:13], v90 offset:18496
	v_mul_f32_e32 v98, 0x3e000000, v18
	v_mfma_f32_16x16x32_bf16 v[22:25], v[22:25], v[50:53], v[14:17]
	v_mul_f32_e32 v99, 0x3e000000, v21
	ds_read_b128 v[110:113], v90 offset:25408
	s_nop 1
	v_mul_f32_e32 v14, 0x3e000000, v19
	v_max3_f32 v77, v77, v98, v14
	s_waitcnt lgkmcnt(2)
	v_mfma_f32_16x16x32_bf16 v[6:9], v[6:9], v[2:5], 0
	ds_read_b128 v[14:17], v90 offset:20736
	v_mul_f32_e32 v98, 0x3e000000, v20
	v_max3_f32 v77, v77, v98, v99
	s_waitcnt lgkmcnt(2)
	v_mfma_f32_16x16x32_bf16 v[10:13], v[10:13], v[50:53], v[6:9]
	v_mul_f32_e32 v98, 0x3e000000, v22
	v_mul_f32_e32 v99, 0x3e000000, v23
	v_max3_f32 v77, v77, v98, v99
	ds_read_b128 v[6:9], v90 offset:20800
	s_waitcnt lgkmcnt(1)
	v_mfma_f32_16x16x32_bf16 v[14:17], v[14:17], v[2:5], 0
	ds_read_b128 v[98:101], v90 offset:23040
	v_mul_f32_e32 v102, 0x3e000000, v24
	v_mul_f32_e32 v103, 0x3e000000, v25
	s_waitcnt lgkmcnt(1)
	v_mfma_f32_16x16x32_bf16 v[14:17], v[6:9], v[50:53], v[14:17]
	ds_read_b128 v[6:9], v90 offset:23104
	v_max3_f32 v77, v77, v102, v103
	ds_read_b128 v[102:105], v90 offset:25344
	s_waitcnt lgkmcnt(2)
	v_mfma_f32_16x16x32_bf16 v[98:101], v[98:101], v[2:5], 0
	v_mul_f32_e32 v114, 0x3e000000, v10
	v_mul_f32_e32 v115, 0x3e000000, v11
	v_mul_f32_e32 v116, 0x3e000000, v12
	s_waitcnt lgkmcnt(1)
	v_mfma_f32_16x16x32_bf16 v[6:9], v[6:9], v[50:53], v[98:101]
	v_mul_f32_e32 v117, 0x3e000000, v13
	v_max3_f32 v77, v77, v114, v115
	v_mul_f32_e32 v118, 0x3e000000, v14
	v_mul_f32_e32 v119, 0x3e000000, v15
	s_waitcnt lgkmcnt(0)
	v_mfma_f32_16x16x32_bf16 v[2:5], v[102:105], v[2:5], 0
	v_max3_f32 v77, v77, v116, v117
	v_mul_f32_e32 v90, 0x3e000000, v16
	v_mul_f32_e32 v98, 0x3e000000, v17
	v_max3_f32 v77, v77, v118, v119
	v_mul_f32_e32 v99, 0x3e000000, v6
	v_mul_f32_e32 v100, 0x3e000000, v7
	v_max3_f32 v77, v77, v90, v98
	v_mul_f32_e32 v101, 0x3e000000, v8
	v_mul_f32_e32 v102, 0x3e000000, v9
	v_max3_f32 v77, v77, v99, v100
	v_mfma_f32_16x16x32_bf16 v[2:5], v[110:113], v[50:53], v[2:5]
	v_max3_f32 v77, v77, v101, v102
	v_lshl_add_u64 v[248:249], v[78:79], 0, 0
	v_lshl_add_u64 v[238:239], v[80:81], 0, 0
	global_load_dwordx4 v[98:101], v[78:79], off offset:128
	global_load_dwordx4 v[102:105], v[80:81], off offset:128
	global_load_dword v250, v[248:249], off offset:256
	global_load_dword v251, v[238:239], off offset:256
	s_waitcnt vmcnt(7)
	ds_write_b128 v73, v[94:97]
	s_waitcnt vmcnt(6)
	ds_write_b128 v73, v[106:109] offset:9216
	s_nop 0
	v_mul_f32_e32 v50, 0x3e000000, v2
	v_mul_f32_e32 v51, 0x3e000000, v3
	v_mul_f32_e32 v52, 0x3e000000, v4
	v_mul_f32_e32 v53, 0x3e000000, v5
	v_max3_f32 v50, v77, v50, v51
	v_max3_f32 v51, v50, v52, v53
	v_cndmask_b32_e32 v50, v82, v83, vcc
	v_lshlrev_b32_e32 v50, 2, v50
	ds_bpermute_b32 v52, v50, v51
	v_cmp_lt_i32_e32 vcc, v85, v84
	s_waitcnt lgkmcnt(0)
	s_barrier
; #define LAS __attribute__((address_space(3)))
; __device__ __forceinline__ unsigned cvt_pk_bf16(float lo, float hi) { const float __attribute__((ext_vector_type(2))) v = {lo, hi}; return __builtin_bit_cast(unsigned, __builtin_convertvector(v, bf16x2_t)); }
; template <bool LOCAL>
; __device__ __forceinline__ void na_unit(const bf16* P, const bf16* VT, bf16* YCAT, const LAS float* rpb_l, LAS bf16* buf, int b, int gr, int hp, int qblk, int tid) {
;     ...
;             if (sidx == NCH - 1) { m = fmaxf(m, __shfl_xor(m, 16)); m = fmaxf(m, __shfl_xor(m, 32)); }
;         } else {
;             const int c = sidx - NCH;
;             if (LOCAL && c < 8) {
;                 float p[8];
; #pragma unroll
;                 for (int e = 0; e < 4; ++e) { p[e] = __expf(sl[2 * (c < 8 ? c : 0)][e] - m); p[4 + e] = __expf(sl[2 * (c < 8 ? c : 0) + 1][e] - m); }
; #pragma unroll
;                 for (int e = 0; e < 8; ++e) lsum += p[e];
;                 const bf16x8 pf = __builtin_bit_cast(bf16x8, (v4u){pg8::cvt_pk_bf16(p[0], p[1]), pg8::cvt_pk_bf16(p[2], p[3]), pg8::cvt_pk_bf16(p[4], p[5]), pg8::cvt_pk_bf16(p[6], p[7])});
; #pragma unroll
;                 for (int dt = 0; dt < 4; ++dt) { const LAS bf16* vp = cb + (16 * dt + fr) * 72 + kc0 + 4 * fq;
;                     o[dt] = __builtin_amdgcn_mfma_f32_16x16x32_bf16(frag44(vp, vp + 16), pf, o[dt], 0, 0, 0); }
;             } else {
;                 const int cc = c - NLOC;
; #pragma unroll
;                 for (int p2 = 0; p2 < 2; ++p2) {
;                     float p[8];
; #pragma unroll
;                     for (int e = 0; e < 4; ++e) { p[e] = __expf(sc[4 * (cc >= 0 ? cc : 0) + 2 * p2][e] - m); p[4 + e] = __expf(sc[4 * (cc >= 0 ? cc : 0) + 2 * p2 + 1][e] - m); }
; #pragma unroll
;                     for (int e = 0; e < 8; ++e) lsum += p[e];
;                     const bf16x8 pf = __builtin_bit_cast(bf16x8, (v4u){pg8::cvt_pk_bf16(p[0], p[1]), pg8::cvt_pk_bf16(p[2], p[3]), pg8::cvt_pk_bf16(p[4], p[5]), pg8::cvt_pk_bf16(p[6], p[7])});
; #pragma unroll
;                     for (int dt = 0; dt < 4; ++dt) { const LAS bf16* vp = cb + (16 * dt + fr) * 72 + 32 * p2 + 4 * fq;
;                         o[dt] = __builtin_amdgcn_mfma_f32_16x16x32_bf16(frag44(vp, vp + 16), pf, o[dt], 0, 0, 0); }
;                 }
;             }
;         }
;         if (sidx + 1 < 2 * NCH) NA_STORE(sidx + 1);
;         __syncthreads();
	v_max_f32_e32 v52, v52, v52
	v_max_f32_e32 v52, v51, v52
	v_cndmask_b32_e32 v51, v82, v85, vcc
	v_lshlrev_b32_e32 v51, 2, v51
	ds_bpermute_b32 v53, v51, v52
	s_waitcnt lgkmcnt(0)
	v_max_f32_e32 v53, v53, v53
	v_max_f32_e32 v77, v52, v53
	v_fma_f32 v52, v62, s72, -v77
	v_fma_f32 v64, v64, s72, -v77
	v_mul_f32_e32 v52, 0x3fb8aa3b, v52
	v_fma_f32 v62, v63, s72, -v77
	v_mul_f32_e32 v64, 0x3fb8aa3b, v64
	v_fma_f32 v65, v65, s72, -v77
	v_exp_f32_e32 v53, v52
	v_fma_f32 v52, v66, s72, -v77
	v_mul_f32_e32 v62, 0x3fb8aa3b, v62
	v_exp_f32_e32 v66, v64
	v_fma_f32 v64, v68, s72, -v77
	v_mul_f32_e32 v65, 0x3fb8aa3b, v65
	v_add3_u32 v68, v86, v76, v87
	v_exp_f32_e32 v63, v62
	v_fma_f32 v62, v67, s72, -v77
	v_exp_f32_e32 v67, v65
	v_fma_f32 v65, v69, s72, -v77
	v_add_u32_e32 v69, 0x800, v68
	v_add_u32_e32 v90, 0x1000, v68
	v_add_u32_e32 v134, 0x1800, v68
	ds_read2_b64 v[94:97], v68 offset1:4
	ds_read2_b64 v[110:113], v69 offset0:32 offset1:36
	ds_read2_b64 v[114:117], v90 offset0:64 offset1:68
	ds_read2_b64 v[118:121], v134 offset0:96 offset1:100
	v_mul_f32_e32 v52, 0x3fb8aa3b, v52
	v_mul_f32_e32 v62, 0x3fb8aa3b, v62
	v_mul_f32_e32 v64, 0x3fb8aa3b, v64
	v_mul_f32_e32 v65, 0x3fb8aa3b, v65
	v_exp_f32_e32 v52, v52
	v_exp_f32_e32 v62, v62
	v_exp_f32_e32 v64, v64
	v_exp_f32_e32 v65, v65
	v_cvt_pk_bf16_f32 v106, v53, v63
	v_cvt_pk_bf16_f32 v107, v66, v67
	v_cvt_pk_bf16_f32 v108, v52, v62
	v_cvt_pk_bf16_f32 v109, v64, v65
	v_fma_f32 v58, v58, s72, -v77
	v_fma_f32 v54, v54, s72, -v77
	s_waitcnt lgkmcnt(3)
	v_mfma_f32_16x16x32_bf16 v[94:97], v[94:97], v[106:109], 0
	v_fma_f32 v59, v59, s72, -v77
	v_fma_f32 v55, v55, s72, -v77
	v_fma_f32 v60, v60, s72, -v77
	s_waitcnt lgkmcnt(2)
	v_mfma_f32_16x16x32_bf16 v[110:113], v[110:113], v[106:109], 0
	v_fma_f32 v56, v56, s72, -v77
	v_fma_f32 v61, v61, s72, -v77
	v_fma_f32 v57, v57, s72, -v77
	s_waitcnt lgkmcnt(1)
	v_mfma_f32_16x16x32_bf16 v[114:117], v[114:117], v[106:109], 0
	v_mul_f32_e32 v58, 0x3fb8aa3b, v58
	v_mul_f32_e32 v54, 0x3fb8aa3b, v54
	v_mul_f32_e32 v59, 0x3fb8aa3b, v59
	s_waitcnt lgkmcnt(0)
	v_mfma_f32_16x16x32_bf16 v[106:109], v[118:121], v[106:109], 0
	ds_read2_b64 v[118:121], v68 offset0:8 offset1:12
	v_mul_f32_e32 v55, 0x3fb8aa3b, v55
	v_mul_f32_e32 v60, 0x3fb8aa3b, v60
	v_mul_f32_e32 v56, 0x3fb8aa3b, v56
	v_mul_f32_e32 v61, 0x3fb8aa3b, v61
	v_mul_f32_e32 v57, 0x3fb8aa3b, v57
	v_exp_f32_e32 v58, v58
	v_exp_f32_e32 v54, v54
	v_exp_f32_e32 v59, v59
	v_exp_f32_e32 v55, v55
	v_exp_f32_e32 v60, v60
	v_exp_f32_e32 v56, v56
	v_exp_f32_e32 v61, v61
	v_exp_f32_e32 v57, v57
	v_cvt_pk_bf16_f32 v122, v58, v59
	v_cvt_pk_bf16_f32 v124, v54, v55
	v_cvt_pk_bf16_f32 v123, v60, v61
	v_cvt_pk_bf16_f32 v125, v56, v57
	v_fma_f32 v42, v42, s72, -v77
	v_mul_f32_e32 v42, 0x3fb8aa3b, v42
	s_waitcnt lgkmcnt(0)
	v_mfma_f32_16x16x32_bf16 v[94:97], v[118:121], v[122:125], v[94:97]
	ds_read2_b64 v[118:121], v69 offset0:40 offset1:44
	v_fma_f32 v46, v46, s72, -v77
	v_mul_f32_e32 v46, 0x3fb8aa3b, v46
	s_waitcnt lgkmcnt(0)
	v_mfma_f32_16x16x32_bf16 v[110:113], v[118:121], v[122:125], v[110:113]
	ds_read2_b64 v[118:121], v90 offset0:72 offset1:76
	v_add_u32_e32 v136, 0x5000, v68
	v_fma_f32 v26, v26, s72, -v77
	s_waitcnt lgkmcnt(0)
	v_mfma_f32_16x16x32_bf16 v[114:117], v[118:121], v[122:125], v[114:117]
	ds_read2_b64 v[118:121], v134 offset0:104 offset1:108
	v_lshl_add_u64 v[248:249], v[78:79], 0, 0
	v_lshl_add_u64 v[238:239], v[80:81], 0, 0
	global_load_dwordx4 v[126:129], v[78:79], off offset:256
	global_load_dwordx4 v[130:133], v[80:81], off offset:256
	global_load_dword v250, v[248:249], off offset:384
	global_load_dword v251, v[238:239], off offset:384
	s_waitcnt vmcnt(7)
	ds_write_b128 v73, v[98:101] offset:18432
	s_waitcnt vmcnt(6)
	ds_write_b128 v73, v[102:105] offset:27648
	s_waitcnt lgkmcnt(2)
	v_mfma_f32_16x16x32_bf16 v[106:109], v[118:121], v[122:125], v[106:109]
	v_exp_f32_e32 v119, v42
	v_fma_f32 v42, v47, s72, -v77
	v_mul_f32_e32 v42, 0x3fb8aa3b, v42
	v_exp_f32_e32 v120, v42
	v_fma_f32 v42, v43, s72, -v77
	v_mul_f32_e32 v42, 0x3fb8aa3b, v42
	v_exp_f32_e32 v121, v42
	v_fma_f32 v42, v48, s72, -v77
	v_mul_f32_e32 v42, 0x3fb8aa3b, v42
	v_exp_f32_e32 v122, v42
	v_fma_f32 v42, v44, s72, -v77
	v_mul_f32_e32 v42, 0x3fb8aa3b, v42
	v_add_u32_e32 v124, 0x4800, v68
	s_waitcnt lgkmcnt(0)
	s_barrier
; #define LAS __attribute__((address_space(3)))
; __device__ __forceinline__ unsigned cvt_pk_bf16(float lo, float hi) { const float __attribute__((ext_vector_type(2))) v = {lo, hi}; return __builtin_bit_cast(unsigned, __builtin_convertvector(v, bf16x2_t)); }
; #define NA_STORE(sidx) do { LAS bf16* d_ = buf + ((sidx) & 1) * 9216; _Pragma("unroll") for (int q_ = 0; q_ < 2; ++q_) *(LAS v4u*)(d_ + q_ * 4608 + lrow * 72 + lseg * 8) = ld[(sidx) & 1][q_]; } while (0)
; template <bool LOCAL>
; __device__ __forceinline__ void na_unit(const bf16* P, const bf16* VT, bf16* YCAT, const LAS float* rpb_l, LAS bf16* buf, int b, int gr, int hp, int qblk, int tid) {
;     ...
;             } else {
;                 const int cc = c - NLOC;
; #pragma unroll
;                 for (int p2 = 0; p2 < 2; ++p2) {
;                     float p[8];
; #pragma unroll
;                     for (int e = 0; e < 4; ++e) { p[e] = __expf(sc[4 * (cc >= 0 ? cc : 0) + 2 * p2][e] - m); p[4 + e] = __expf(sc[4 * (cc >= 0 ? cc : 0) + 2 * p2 + 1][e] - m); }
; #pragma unroll
;                     for (int e = 0; e < 8; ++e) lsum += p[e];
;                     const bf16x8 pf = __builtin_bit_cast(bf16x8, (v4u){pg8::cvt_pk_bf16(p[0], p[1]), pg8::cvt_pk_bf16(p[2], p[3]), pg8::cvt_pk_bf16(p[4], p[5]), pg8::cvt_pk_bf16(p[6], p[7])});
; #pragma unroll
;                     for (int dt = 0; dt < 4; ++dt) { const LAS bf16* vp = cb + (16 * dt + fr) * 72 + 32 * p2 + 4 * fq;
;                         o[dt] = __builtin_amdgcn_mfma_f32_16x16x32_bf16(frag44(vp, vp + 16), pf, o[dt], 0, 0, 0); }
;                 }
;             }
;         }
;         if (sidx + 1 < 2 * NCH) NA_STORE(sidx + 1);
;         __syncthreads();
	v_exp_f32_e32 v118, v46
	v_exp_f32_e32 v123, v42
	v_fma_f32 v42, v49, s72, -v77
	ds_read2_b64 v[46:49], v124 offset1:4
	v_mul_f32_e32 v42, 0x3fb8aa3b, v42
	v_exp_f32_e32 v125, v42
	v_fma_f32 v42, v45, s72, -v77
	v_mul_f32_e32 v42, 0x3fb8aa3b, v42
	v_exp_f32_e32 v135, v42
	v_cvt_pk_bf16_f32 v42, v118, v120
	v_cvt_pk_bf16_f32 v43, v122, v125
	v_cvt_pk_bf16_f32 v44, v119, v121
	v_cvt_pk_bf16_f32 v45, v123, v135
	v_mul_f32_e32 v26, 0x3fb8aa3b, v26
	v_fma_f32 v34, v34, s72, -v77
	s_waitcnt lgkmcnt(0)
	v_mfma_f32_16x16x32_bf16 v[46:49], v[46:49], v[42:45], v[94:97]
	v_mul_f32_e32 v34, 0x3fb8aa3b, v34
	v_fma_f32 v30, v30, s72, -v77
	v_mul_f32_e32 v30, 0x3fb8aa3b, v30
	ds_read2_b64 v[94:97], v136 offset0:32 offset1:36
	s_waitcnt lgkmcnt(0)
	v_mfma_f32_16x16x32_bf16 v[94:97], v[94:97], v[42:45], v[110:113]
	s_nop 2
	v_add_u32_e32 v110, 0x5800, v68
	v_add_u32_e32 v111, 0x6000, v68
	ds_read2_b64 v[98:101], v110 offset0:64 offset1:68
	ds_read2_b64 v[102:105], v111 offset0:96 offset1:100
	s_waitcnt lgkmcnt(1)
	v_mfma_f32_16x16x32_bf16 v[98:101], v[98:101], v[42:45], v[114:117]
	v_fma_f32 v38, v38, s72, -v77
	v_mul_f32_e32 v38, 0x3fb8aa3b, v38
	v_fma_f32 v18, v18, s72, -v77
	s_waitcnt lgkmcnt(0)
	v_mfma_f32_16x16x32_bf16 v[42:45], v[102:105], v[42:45], v[106:109]
	v_mul_f32_e32 v18, 0x3fb8aa3b, v18
	v_fma_f32 v10, v10, s72, -v77
	v_mul_f32_e32 v10, 0x3fb8aa3b, v10
	v_exp_f32_e32 v107, v26
	v_fma_f32 v26, v35, s72, -v77
	v_mul_f32_e32 v26, 0x3fb8aa3b, v26
	v_exp_f32_e32 v108, v26
	v_fma_f32 v26, v27, s72, -v77
	v_mul_f32_e32 v26, 0x3fb8aa3b, v26
	v_exp_f32_e32 v109, v26
	v_fma_f32 v26, v36, s72, -v77
	v_mul_f32_e32 v26, 0x3fb8aa3b, v26
	v_exp_f32_e32 v112, v26
	v_fma_f32 v26, v28, s72, -v77
	v_mul_f32_e32 v26, 0x3fb8aa3b, v26
	v_exp_f32_e32 v106, v34
	v_exp_f32_e32 v113, v26
	v_fma_f32 v26, v37, s72, -v77
	ds_read2_b64 v[34:37], v124 offset0:8 offset1:12
	v_mul_f32_e32 v26, 0x3fb8aa3b, v26
	v_exp_f32_e32 v114, v26
	v_fma_f32 v26, v29, s72, -v77
	v_mul_f32_e32 v26, 0x3fb8aa3b, v26
	v_exp_f32_e32 v115, v26
	v_cvt_pk_bf16_f32 v26, v106, v108
	v_cvt_pk_bf16_f32 v27, v112, v114
	v_cvt_pk_bf16_f32 v28, v107, v109
	v_cvt_pk_bf16_f32 v29, v113, v115
	v_fma_f32 v2, v2, s72, -v77
	v_mul_f32_e32 v2, 0x3fb8aa3b, v2
	s_waitcnt lgkmcnt(0)
	v_mfma_f32_16x16x32_bf16 v[34:37], v[34:37], v[26:29], v[46:49]
	v_fma_f32 v6, v6, s72, -v77
	v_mul_f32_e32 v6, 0x3fb8aa3b, v6
	s_nop 0
	ds_read2_b64 v[46:49], v136 offset0:40 offset1:44
	s_waitcnt lgkmcnt(0)
	v_mfma_f32_16x16x32_bf16 v[46:49], v[46:49], v[26:29], v[94:97]
	s_nop 2
	ds_read2_b64 v[94:97], v110 offset0:72 offset1:76
	s_waitcnt lgkmcnt(0)
	v_mfma_f32_16x16x32_bf16 v[94:97], v[94:97], v[26:29], v[98:101]
	s_nop 2
	ds_read2_b64 v[98:101], v111 offset0:104 offset1:108
	global_load_dwordx4 v[102:105], v[78:79], off offset:384
	s_nop 0
	global_load_dwordx4 v[78:81], v[80:81], off offset:384
	s_waitcnt vmcnt(5)
	ds_write_b128 v73, v[126:129]
	s_waitcnt vmcnt(4)
	ds_write_b128 v73, v[130:133] offset:9216
	s_waitcnt lgkmcnt(2)
	v_mfma_f32_16x16x32_bf16 v[26:29], v[98:101], v[26:29], v[42:45]
	v_exp_f32_e32 v99, v30
	v_fma_f32 v30, v39, s72, -v77
	v_mul_f32_e32 v30, 0x3fb8aa3b, v30
	v_exp_f32_e32 v100, v30
	v_fma_f32 v30, v31, s72, -v77
	v_mul_f32_e32 v30, 0x3fb8aa3b, v30
	v_exp_f32_e32 v101, v30
	v_fma_f32 v30, v40, s72, -v77
	v_mul_f32_e32 v30, 0x3fb8aa3b, v30
	v_exp_f32_e32 v116, v30
	v_fma_f32 v30, v32, s72, -v77
	v_mul_f32_e32 v30, 0x3fb8aa3b, v30
	s_waitcnt lgkmcnt(0)
	s_barrier
	v_exp_f32_e32 v98, v38
	v_exp_f32_e32 v117, v30
	v_fma_f32 v30, v41, s72, -v77
	ds_read2_b64 v[38:41], v68 offset1:4
	v_mul_f32_e32 v30, 0x3fb8aa3b, v30
	v_exp_f32_e32 v126, v30
	v_fma_f32 v30, v33, s72, -v77
	v_mul_f32_e32 v30, 0x3fb8aa3b, v30
	v_exp_f32_e32 v127, v30
	v_cvt_pk_bf16_f32 v30, v98, v100
	v_cvt_pk_bf16_f32 v31, v116, v126
	v_cvt_pk_bf16_f32 v32, v99, v101
	v_cvt_pk_bf16_f32 v33, v117, v127
	ds_read2_b64 v[42:45], v90 offset0:64 offset1:68
	s_waitcnt lgkmcnt(1)
	v_mfma_f32_16x16x32_bf16 v[34:37], v[38:41], v[30:33], v[34:37]
	ds_read2_b64 v[38:41], v69 offset0:32 offset1:36
	s_waitcnt lgkmcnt(0)
	v_mfma_f32_16x16x32_bf16 v[38:41], v[38:41], v[30:33], v[46:49]
	s_nop 2
	ds_read2_b64 v[46:49], v134 offset0:96 offset1:100
	s_waitcnt lgkmcnt(0)
	v_mfma_f32_16x16x32_bf16 v[26:29], v[46:49], v[30:33], v[26:29]
	v_exp_f32_e32 v46, v18
	v_fma_f32 v18, v22, s72, -v77
	v_mul_f32_e32 v18, 0x3fb8aa3b, v18
	v_exp_f32_e32 v47, v18
	v_fma_f32 v18, v19, s72, -v77
	v_mul_f32_e32 v18, 0x3fb8aa3b, v18
	v_exp_f32_e32 v48, v18
	v_fma_f32 v18, v23, s72, -v77
	v_mul_f32_e32 v18, 0x3fb8aa3b, v18
	v_exp_f32_e32 v49, v18
	v_fma_f32 v18, v20, s72, -v77
	v_mul_f32_e32 v18, 0x3fb8aa3b, v18
	v_mfma_f32_16x16x32_bf16 v[42:45], v[42:45], v[30:33], v[94:97]
	ds_read2_b64 v[30:33], v69 offset0:40 offset1:44
	s_nop 1
	v_exp_f32_e32 v94, v18
	v_fma_f32 v18, v24, s72, -v77
	v_mul_f32_e32 v18, 0x3fb8aa3b, v18
	v_exp_f32_e32 v95, v18
	v_fma_f32 v18, v21, s72, -v77
	v_mul_f32_e32 v22, 0x3fb8aa3b, v18
	ds_read2_b64 v[18:21], v68 offset0:8 offset1:12
	v_exp_f32_e32 v68, v22
	v_fma_f32 v22, v25, s72, -v77
	v_mul_f32_e32 v22, 0x3fb8aa3b, v22
	v_exp_f32_e32 v96, v22
	v_cvt_pk_bf16_f32 v22, v46, v48
	v_cvt_pk_bf16_f32 v23, v94, v68
	v_cvt_pk_bf16_f32 v24, v47, v49
	v_cvt_pk_bf16_f32 v25, v95, v96
	s_waitcnt lgkmcnt(0)
	s_nop 0
	v_mfma_f32_16x16x32_bf16 v[18:21], v[18:21], v[22:25], v[34:37]
	v_mfma_f32_16x16x32_bf16 v[30:33], v[30:33], v[22:25], v[38:41]
	s_nop 1
	ds_read2_b64 v[34:37], v90 offset0:72 offset1:76
	ds_read2_b64 v[38:41], v134 offset0:104 offset1:108
	s_waitcnt lgkmcnt(1)
	v_mfma_f32_16x16x32_bf16 v[34:37], v[34:37], v[22:25], v[42:45]
	s_waitcnt vmcnt(1)
	ds_write_b128 v73, v[102:105] offset:18432
	s_waitcnt vmcnt(0)
	ds_write_b128 v73, v[78:81] offset:27648
	s_waitcnt lgkmcnt(0)
	s_barrier
; #define LAS __attribute__((address_space(3)))
; __device__ __forceinline__ unsigned cvt_pk_bf16(float lo, float hi) { const float __attribute__((ext_vector_type(2))) v = {lo, hi}; return __builtin_bit_cast(unsigned, __builtin_convertvector(v, bf16x2_t)); }
; #define NA_STORE(sidx) do { LAS bf16* d_ = buf + ((sidx) & 1) * 9216; _Pragma("unroll") for (int q_ = 0; q_ < 2; ++q_) *(LAS v4u*)(d_ + q_ * 4608 + lrow * 72 + lseg * 8) = ld[(sidx) & 1][q_]; } while (0)
; template <bool LOCAL>
; __device__ __forceinline__ void na_unit(const bf16* P, const bf16* VT, bf16* YCAT, const LAS float* rpb_l, LAS bf16* buf, int b, int gr, int hp, int qblk, int tid) {
;     ...
;             } else {
;                 const int cc = c - NLOC;
; #pragma unroll
;                 for (int p2 = 0; p2 < 2; ++p2) {
;                     float p[8];
; #pragma unroll
;                     for (int e = 0; e < 4; ++e) { p[e] = __expf(sc[4 * (cc >= 0 ? cc : 0) + 2 * p2][e] - m); p[4 + e] = __expf(sc[4 * (cc >= 0 ? cc : 0) + 2 * p2 + 1][e] - m); }
; #pragma unroll
;                     for (int e = 0; e < 8; ++e) lsum += p[e];
;                     const bf16x8 pf = __builtin_bit_cast(bf16x8, (v4u){pg8::cvt_pk_bf16(p[0], p[1]), pg8::cvt_pk_bf16(p[2], p[3]), pg8::cvt_pk_bf16(p[4], p[5]), pg8::cvt_pk_bf16(p[6], p[7])});
; #pragma unroll
;                     for (int dt = 0; dt < 4; ++dt) { const LAS bf16* vp = cb + (16 * dt + fr) * 72 + 32 * p2 + 4 * fq;
;                         o[dt] = __builtin_amdgcn_mfma_f32_16x16x32_bf16(frag44(vp, vp + 16), pf, o[dt], 0, 0, 0); }
;                 }
;             }
;         }
;         if (sidx + 1 < 2 * NCH) NA_STORE(sidx + 1);
;         __syncthreads();
;     }
;     ...
;     lsum += __shfl_xor(lsum, 16); lsum += __shfl_xor(lsum, 32);
;     const float inv = 1.f / lsum;
;     bf16* op = YCAT + (size_t)(qrow0 + fr) * D + 512 + h * 64 + 4 * fq;
; #pragma unroll
;     for (int dt = 0; dt < 4; ++dt) { v2u w; w.x = pg8::cvt_pk_bf16(o[dt][0] * inv, o[dt][1] * inv); w.y = pg8::cvt_pk_bf16(o[dt][2] * inv, o[dt][3] * inv); *(v2u*)(op + dt * 16) = w; }
	v_mfma_f32_16x16x32_bf16 v[22:25], v[38:41], v[22:25], v[26:29]
	v_exp_f32_e32 v38, v10
	v_fma_f32 v10, v14, s72, -v77
	v_mul_f32_e32 v10, 0x3fb8aa3b, v10
	v_exp_f32_e32 v39, v10
	v_fma_f32 v10, v11, s72, -v77
	v_mul_f32_e32 v10, 0x3fb8aa3b, v10
	v_exp_f32_e32 v40, v10
	v_fma_f32 v10, v15, s72, -v77
	v_mul_f32_e32 v10, 0x3fb8aa3b, v10
	v_exp_f32_e32 v41, v10
	v_fma_f32 v10, v12, s72, -v77
	v_mul_f32_e32 v10, 0x3fb8aa3b, v10
	v_exp_f32_e32 v42, v10
	v_fma_f32 v10, v16, s72, -v77
	v_mul_f32_e32 v10, 0x3fb8aa3b, v10
	v_exp_f32_e32 v43, v10
	v_fma_f32 v10, v13, s72, -v77
	ds_read2_b64 v[26:29], v110 offset0:64 offset1:68
	v_mul_f32_e32 v14, 0x3fb8aa3b, v10
	v_exp_f32_e32 v44, v14
	v_fma_f32 v14, v17, s72, -v77
	v_mul_f32_e32 v14, 0x3fb8aa3b, v14
	v_exp_f32_e32 v45, v14
	v_cvt_pk_bf16_f32 v14, v38, v40
	v_cvt_pk_bf16_f32 v15, v42, v44
	v_cvt_pk_bf16_f32 v16, v39, v41
	v_cvt_pk_bf16_f32 v17, v43, v45
	ds_read2_b64 v[10:13], v124 offset1:4
	v_mov_b32_e32 v73, v71
	s_waitcnt lgkmcnt(1)
	v_mfma_f32_16x16x32_bf16 v[26:29], v[26:29], v[14:17], v[34:37]
	s_nop 2
	v_add_f32_e32 v34, 0, v53
	v_add_f32_e32 v34, v63, v34
	v_add_f32_e32 v34, v66, v34
	v_add_f32_e32 v34, v67, v34
	v_add_f32_e32 v34, v52, v34
	v_add_f32_e32 v34, v62, v34
	v_add_f32_e32 v34, v64, v34
	v_add_f32_e32 v34, v65, v34
	v_add_f32_e32 v34, v58, v34
	v_add_f32_e32 v34, v59, v34
	v_add_f32_e32 v34, v60, v34
	v_add_f32_e32 v34, v61, v34
	v_add_f32_e32 v34, v54, v34
	v_add_f32_e32 v34, v55, v34
	v_add_f32_e32 v34, v56, v34
	v_add_f32_e32 v34, v57, v34
	s_waitcnt lgkmcnt(0)
	v_mfma_f32_16x16x32_bf16 v[10:13], v[10:13], v[14:17], v[18:21]
	v_add_f32_e32 v34, v118, v34
	v_add_f32_e32 v34, v120, v34
	v_add_f32_e32 v34, v122, v34
	ds_read2_b64 v[18:21], v136 offset0:32 offset1:36
	v_add_f32_e32 v34, v125, v34
	v_add_f32_e32 v34, v119, v34
	v_add_f32_e32 v34, v121, v34
	v_add_f32_e32 v34, v123, v34
	v_add_f32_e32 v34, v135, v34
	v_add_f32_e32 v34, v106, v34
	s_waitcnt lgkmcnt(0)
	v_mfma_f32_16x16x32_bf16 v[18:21], v[18:21], v[14:17], v[30:33]
	v_add_f32_e32 v34, v108, v34
	s_nop 1
	ds_read2_b64 v[30:33], v111 offset0:96 offset1:100
	v_add_f32_e32 v34, v112, v34
	v_add_f32_e32 v34, v114, v34
	v_add_f32_e32 v34, v107, v34
	v_add_f32_e32 v34, v109, v34
	v_add_f32_e32 v34, v113, v34
	v_add_f32_e32 v34, v115, v34
	v_add_f32_e32 v34, v98, v34
	v_add_f32_e32 v34, v100, v34
	s_waitcnt lgkmcnt(0)
	v_mfma_f32_16x16x32_bf16 v[14:17], v[30:33], v[14:17], v[22:25]
	v_add_f32_e32 v34, v116, v34
	v_add_f32_e32 v34, v126, v34
	v_add_f32_e32 v34, v99, v34
	v_exp_f32_e32 v23, v2
	v_fma_f32 v2, v7, s72, -v77
	v_mul_f32_e32 v2, 0x3fb8aa3b, v2
	v_exp_f32_e32 v24, v2
	v_fma_f32 v2, v3, s72, -v77
	v_mul_f32_e32 v2, 0x3fb8aa3b, v2
	v_add_f32_e32 v34, v101, v34
	v_exp_f32_e32 v25, v2
	v_fma_f32 v2, v8, s72, -v77
	v_add_f32_e32 v34, v117, v34
	v_mul_f32_e32 v2, 0x3fb8aa3b, v2
	v_add_f32_e32 v34, v127, v34
	v_exp_f32_e32 v30, v2
	v_fma_f32 v2, v4, s72, -v77
	v_add_f32_e32 v34, v46, v34
	v_mul_f32_e32 v2, 0x3fb8aa3b, v2
	v_add_f32_e32 v34, v48, v34
	v_exp_f32_e32 v22, v6
	v_exp_f32_e32 v31, v2
	v_fma_f32 v2, v9, s72, -v77
	ds_read2_b64 v[6:9], v124 offset0:8 offset1:12
	v_add_f32_e32 v34, v94, v34
	v_mul_f32_e32 v2, 0x3fb8aa3b, v2
	v_add_f32_e32 v34, v68, v34
	v_exp_f32_e32 v32, v2
	v_fma_f32 v2, v5, s72, -v77
	v_add_f32_e32 v34, v47, v34
	v_mul_f32_e32 v2, 0x3fb8aa3b, v2
	v_add_f32_e32 v34, v49, v34
	v_exp_f32_e32 v33, v2
	v_add_f32_e32 v34, v95, v34
	v_add_f32_e32 v34, v96, v34
	v_add_f32_e32 v34, v38, v34
	v_add_f32_e32 v34, v40, v34
	v_cvt_pk_bf16_f32 v2, v22, v24
	v_cvt_pk_bf16_f32 v3, v30, v32
	v_cvt_pk_bf16_f32 v4, v23, v25
	v_cvt_pk_bf16_f32 v5, v31, v33
	v_add_f32_e32 v34, v42, v34
	v_add_f32_e32 v34, v44, v34
	s_waitcnt lgkmcnt(0)
	v_mfma_f32_16x16x32_bf16 v[6:9], v[6:9], v[2:5], v[10:13]
	v_add_f32_e32 v34, v39, v34
	v_add_f32_e32 v34, v41, v34
	v_add_f32_e32 v34, v43, v34
	ds_read2_b64 v[10:13], v136 offset0:40 offset1:44
	v_add_f32_e32 v34, v45, v34
	v_add_f32_e32 v22, v22, v34
	v_add_f32_e32 v22, v24, v22
	v_add_f32_e32 v22, v30, v22
	v_add_f32_e32 v22, v32, v22
	s_waitcnt lgkmcnt(0)
	v_mfma_f32_16x16x32_bf16 v[10:13], v[10:13], v[2:5], v[18:21]
	s_nop 2
	ds_read2_b64 v[18:21], v110 offset0:72 offset1:76
	v_add_f32_e32 v22, v23, v22
	v_add_f32_e32 v22, v25, v22
	v_add_f32_e32 v22, v31, v22
	v_add_f32_e32 v30, v33, v22
	ds_bpermute_b32 v31, v50, v30
	ds_read2_b64 v[22:25], v111 offset0:104 offset1:108
	s_waitcnt lgkmcnt(2)
	v_mfma_f32_16x16x32_bf16 v[18:21], v[18:21], v[2:5], v[26:29]
	v_mov_b32_e32 v77, v71
	s_waitcnt lgkmcnt(1)
	s_nop 0
	v_add_f32_e32 v26, v30, v31
	ds_bpermute_b32 v27, v51, v26
	s_waitcnt lgkmcnt(1)
	v_mfma_f32_16x16x32_bf16 v[14:17], v[22:25], v[2:5], v[14:17]
	s_waitcnt lgkmcnt(0)
	v_add_f32_e32 v2, v26, v27
	v_div_scale_f32 v3, s[0:1], v2, v2, 1.0
	v_rcp_f32_e32 v4, v3
	s_barrier
	s_mov_b64 s[0:1], 0
	v_fma_f32 v5, -v3, v4, 1.0
	v_fmac_f32_e32 v4, v5, v4
	v_div_scale_f32 v5, vcc, 1.0, v2, 1.0
	v_mul_f32_e32 v22, v5, v4
	v_fma_f32 v23, -v3, v22, v5
	v_fmac_f32_e32 v22, v23, v4
	v_fma_f32 v3, -v3, v22, v5
	v_div_fmas_f32 v3, v3, v4, v22
	v_div_fixup_f32 v22, v3, v2, 1.0
	v_lshlrev_b64 v[2:3], 11, v[72:73]
	v_lshl_add_u64 v[2:3], s[10:11], 0, v[2:3]
	v_lshl_add_u64 v[2:3], v[2:3], 0, v[74:75]
	v_pk_mul_f32 v[6:7], v[6:7], v[22:23] op_sel_hi:[1,0]
	v_pk_mul_f32 v[8:9], v[8:9], v[22:23] op_sel_hi:[1,0]
	v_lshl_add_u64 v[4:5], v[2:3], 0, v[76:77]
	v_cvt_pk_bf16_f32 v6, v6, v7
	v_cvt_pk_bf16_f32 v7, v8, v9
	global_store_dwordx2 v[4:5], v[6:7], off offset:1024
	v_pk_mul_f32 v[6:7], v[10:11], v[22:23] op_sel_hi:[1,0]
	v_pk_mul_f32 v[8:9], v[12:13], v[22:23] op_sel_hi:[1,0]
	v_cvt_pk_bf16_f32 v6, v6, v7
	v_cvt_pk_bf16_f32 v7, v8, v9
	global_store_dwordx2 v[4:5], v[6:7], off offset:1056
	v_pk_mul_f32 v[6:7], v[18:19], v[22:23] op_sel_hi:[1,0]
	v_pk_mul_f32 v[8:9], v[20:21], v[22:23] op_sel_hi:[1,0]
	v_cvt_pk_bf16_f32 v6, v6, v7
	v_cvt_pk_bf16_f32 v7, v8, v9
	v_lshl_add_u64 v[2:3], v[4:5], 0, s[12:13]
	global_store_dwordx2 v[4:5], v[6:7], off offset:1088
	v_pk_mul_f32 v[4:5], v[14:15], v[22:23] op_sel_hi:[1,0]
	v_pk_mul_f32 v[6:7], v[16:17], v[22:23] op_sel_hi:[1,0]
	v_cvt_pk_bf16_f32 v4, v4, v5

; #define LAS __attribute__((address_space(3)))
; template <bool LOCAL>
; __device__ __forceinline__ void na_unit(const bf16* P, const bf16* VT, bf16* YCAT, const LAS float* rpb_l, LAS bf16* buf, int b, int gr, int hp, int qblk, int tid) {
;     typedef pg8::bf16x8 bf16x8;
;     constexpr int NCH = LOCAL ? 12 : 4, NLOC = LOCAL ? 8 : 0;
;     const int lane = tid & 63, wv = tid >> 6, fr = lane & 15, fq = lane >> 4, hh = wv >> 2, qb = wv & 3, h = 2 * hp + hh;
;     const int qrow0 = LOCAL ? NCTX + b * SEQ + gr * 64 + 16 * qb : b * CTXL + qblk * 64 + 16 * qb;
;     const int r0 = min(max(gr - 4, 0), 24);
;     const int kc0 = qb == 0 ? 0 : qb == 1 ? 8 : qb == 2 ? 24 : 32;
;     const int qcol = 16 * qb + fr, cs = min(max(qcol - 8, 0), 48);
;     const LAS float* rpb = rpb_l + h * 15 * 31;
;     v4u ld[2][2];
;     const int lrow = (tid >> 3) & 63, lseg = tid & 7;
;     ...
;     bf16x8 qf[2];
; #pragma unroll
;     for (int ks = 0; ks < 2; ++ks) qf[ks] = *(const bf16x8*)(P + (size_t)(qrow0 + fr) * DINP + h * 64 + 32 * ks + 8 * fq);
;     f32x4 sl[16], sc[16];
;     float m = -1.0e30f, lsum = 0.f;
;     f32x4 o[4];
; #pragma unroll
;     for (int dt = 0; dt < 4; ++dt) o[dt] = (f32x4){0.f, 0.f, 0.f, 0.f};
;     NA_ISSUE(0); NA_ISSUE(1); NA_STORE(0);
;     __syncthreads();
; #pragma unroll
;     for (int sidx = 0; sidx < 2 * NCH; ++sidx) {
;         if (sidx + 2 < 2 * NCH) NA_ISSUE(sidx + 2);
;         const LAS bf16* cb = buf + (sidx & 1) * 9216 + hh * 4608;
;         if (sidx < NCH) {
;             const int c = sidx;
;             if (LOCAL && c < 8) {
; #pragma unroll
;                 for (int t2 = 0; t2 < 2; ++t2) {
;                     const LAS bf16* kp = cb + (kc0 + 16 * t2 + fr) * 72 + 8 * fq;
;                     f32x4 acc = {0.f, 0.f, 0.f, 0.f};
;                     acc = __builtin_amdgcn_mfma_f32_16x16x32_bf16(*(const LAS bf16x8*)(kp), qf[0], acc, 0, 0, 0);
;                     acc = __builtin_amdgcn_mfma_f32_16x16x32_bf16(*(const LAS bf16x8*)(kp + 32), qf[1], acc, 0, 0, 0);
;                     const LAS float* rb = rpb + (r0 + c - gr + 7) * 31 + 15 - qcol;
; #pragma unroll
;                     for (int e = 0; e < 4; ++e) { const int kcol = kc0 + 16 * t2 + 4 * fq + e; const bool ok = (kcol >= cs) && (kcol < cs + 16);
;                         const float sv = ok ? acc[e] * 0.125f + rb[ok ? kcol : qcol] : -1.0e30f; acc[e] = sv; m = fmaxf(m, sv); }
.LBB0_645:
	s_or_b64 exec, exec, s[0:1]
	s_bfe_u32 s19, s76, 0x50002
	v_sub_u32_e64 v3, s19, 4 clamp
	s_ashr_i32 s17, s76, 7
	v_readfirstlane_b32 s0, v3
	s_lshl_b32 s26, s17, 11
	s_min_u32 s20, s0, 24
	s_add_i32 s14, s26, 0x1000
	s_lshl_b32 s15, s20, 6
	s_or_b32 s16, s15, s14
	v_mov_b64_e32 v[18:19], s[8:9]
	v_and_b32_e32 v32, 7, v93
	v_or_b32_e32 v3, s16, v88
	s_and_b32 s18, s76, 3
	v_mad_i64_i32 v[4:5], s[0:1], v3, s70, v[18:19]
	v_lshlrev_b32_e32 v26, 4, v32
	v_mov_b32_e32 v27, v71
	v_lshl_add_u64 v[4:5], v[4:5], 0, v[26:27]
	s_lshl_b32 s2, s18, 8
	v_lshl_add_u64 v[4:5], v[4:5], 0, s[2:3]
	global_load_dwordx4 v[10:13], v[4:5], off offset:1024
	global_load_dwordx4 v[14:17], v[4:5], off offset:1152
	s_lshl_b32 s0, s19, 6
	v_lshl_or_b32 v31, v2, 4, v89
	v_lshl_add_u32 v33, s18, 1, v92
	s_or_b32 s0, s14, s0
	v_mad_u32_u24 v2, v88, s71, 0
	v_lshlrev_b32_e32 v72, 6, v33
	s_add_i32 s50, s26, 0x1040
	v_or_b32_e32 v74, s0, v31
	v_add_u32_e32 v75, v2, v26
	v_ashrrev_i32_e32 v73, 31, v72
	v_or_b32_e32 v4, s50, v88
	v_mad_i64_i32 v[2:3], s[0:1], v74, s70, v[18:19]
	v_add_u32_e32 v4, s15, v4
	v_lshl_add_u64 v[2:3], v[72:73], 1, v[2:3]
	v_mad_i64_i32 v[4:5], s[0:1], v4, s70, v[18:19]
	v_lshl_add_u64 v[2:3], v[2:3], 0, v[70:71]
	v_lshl_add_u64 v[20:21], v[4:5], 0, v[26:27]
	global_load_dwordx4 v[6:9], v[2:3], off
	s_nop 0
	global_load_dwordx4 v[2:5], v[2:3], off offset:64
	s_or_b32 s14, s26, s15
	s_addk_i32 s14, 0x1080
	v_or_b32_e32 v24, s14, v88
	v_mad_i64_i32 v[28:29], s[0:1], v24, s70, v[18:19]
	v_lshl_add_u64 v[26:27], v[28:29], 0, v[26:27]
	v_lshl_add_u64 v[22:23], v[20:21], 0, s[2:3]
	v_lshl_add_u64 v[26:27], v[26:27], 0, s[2:3]
	s_mov_b32 s100, 0x60000
	s_mov_b32 s101, 0
	v_lshl_add_u64 v[248:249], v[22:23], 0, s[100:101]
	global_load_dwordx4 v[18:21], v[22:23], off offset:1024
	s_nop 0
	global_load_dwordx4 v[22:25], v[22:23], off offset:1152
	global_load_dword v250, v[248:249], off offset:1024
	global_load_dword v251, v[248:249], off offset:1152
	v_add_u32_e32 v30, v86, v70
	v_add_u32_e32 v34, v90, v89
	v_mad_u32_u24 v36, v34, s71, v30
	s_movk_i32 s0, 0x744
	v_mul_lo_u32 v33, v33, s0
	s_sub_i32 s0, s20, s19
	s_mulk_i32 s0, 0x7c
	v_sub_u32_e64 v35, v31, 8 clamp
	s_add_i32 s0, s0, 0
	v_min_u32_e32 v35, 48, v35
	v_lshlrev_b32_e32 v77, 2, v91
	v_add_u32_e32 v33, s0, v33
	v_lshlrev_b32_e32 v31, 2, v31
	v_sub_u32_e32 v31, v33, v31
	v_add_u32_e32 v33, v90, v77
	v_cmp_ge_u32_e32 vcc, v33, v35
	v_mov_b32_e32 v91, 0xf149f2ca
	v_lshl_add_u32 v31, v33, 2, v31
	v_mov_b32_e32 v92, 0xf149f2ca
	s_waitcnt vmcnt(7)
	ds_write_b128 v75, v[10:13]
	s_waitcnt vmcnt(6)
	ds_write_b128 v75, v[14:17] offset:9216
	s_waitcnt lgkmcnt(0)
	s_barrier
	ds_read_b32 v240, v31 offset:37792
	ds_read_b32 v241, v31 offset:37796
	ds_read_b32 v242, v31 offset:37800
	ds_read_b32 v243, v31 offset:37804
	ds_read_b32 v244, v31 offset:37856
	ds_read_b32 v245, v31 offset:37860
	ds_read_b32 v246, v31 offset:37864
	ds_read_b32 v247, v31 offset:37868
	v_lshl_add_u64 v[248:249], v[26:27], 0, s[100:101]
	global_load_dwordx4 v[10:13], v[26:27], off offset:1024
	global_load_dwordx4 v[14:17], v[26:27], off offset:1152
	global_load_dword v250, v[248:249], off offset:1024
	global_load_dword v251, v[248:249], off offset:1152
	ds_read_b128 v[26:29], v36
	ds_read_b128 v[38:41], v36 offset:64
	s_waitcnt vmcnt(9) lgkmcnt(1)
	v_mfma_f32_16x16x32_bf16 v[26:29], v[26:29], v[6:9], 0
	v_add_u32_e32 v36, 16, v35
	v_cmp_lt_u32_e64 s[0:1], v33, v36
	s_and_b64 s[28:29], vcc, s[0:1]
	s_waitcnt vmcnt(8) lgkmcnt(0)
	v_mfma_f32_16x16x32_bf16 v[26:29], v[38:41], v[2:5], v[26:29]
	s_nop 2
	s_waitcnt lgkmcnt(0)
	s_nop 3
	v_fmac_f32_e32 v240, 0x3e000000, v26
	v_cndmask_b32_e64 v92, v92, v240, s[28:29]
	s_nop 4
	v_or_b32_e32 v26, 1, v33
	v_cmp_ge_u32_e32 vcc, v26, v35
	v_cmp_lt_u32_e64 s[0:1], v26, v36
	s_and_b64 s[30:31], vcc, s[0:1]
	s_nop 2
	s_waitcnt lgkmcnt(0)
	v_fmac_f32_e32 v241, 0x3e000000, v27
	v_cndmask_b32_e64 v91, v91, v241, s[30:31]
	v_or_b32_e32 v26, 2, v33
	v_cmp_ge_u32_e32 vcc, v26, v35
	v_cmp_lt_u32_e64 s[0:1], v26, v36
	s_and_b64 s[34:35], vcc, s[0:1]
	v_mov_b32_e32 v93, 0xf149f2ca
	v_mov_b32_e32 v94, 0xf149f2ca
	s_nop 2
	s_waitcnt lgkmcnt(0)
	v_fmac_f32_e32 v242, 0x3e000000, v28
	v_cndmask_b32_e64 v94, v94, v242, s[34:35]
	v_or_b32_e32 v26, 3, v33
	v_cmp_ge_u32_e32 vcc, v26, v35
	v_cmp_lt_u32_e64 s[0:1], v26, v36
	s_and_b64 s[36:37], vcc, s[0:1]
	s_nop 2
	s_waitcnt lgkmcnt(0)
	v_fmac_f32_e32 v243, 0x3e000000, v29
	v_cndmask_b32_e64 v93, v93, v243, s[36:37]
	v_add_u32_e32 v37, 16, v90
	v_add_u32_e32 v33, v37, v89
	v_mad_u32_u24 v38, v33, s71, v30
	ds_read_b128 v[26:29], v38
	ds_read_b128 v[38:41], v38 offset:64
	v_add_u32_e32 v37, v37, v77
	v_cmp_ge_u32_e32 vcc, v37, v35
	v_cmp_lt_u32_e64 s[0:1], v37, v36
	s_waitcnt lgkmcnt(1)
	v_mfma_f32_16x16x32_bf16 v[26:29], v[26:29], v[6:9], 0
	s_and_b64 s[38:39], vcc, s[0:1]
	v_mov_b32_e32 v95, 0xf149f2ca
	v_mov_b32_e32 v96, 0xf149f2ca
	s_waitcnt lgkmcnt(0)
	v_mfma_f32_16x16x32_bf16 v[26:29], v[38:41], v[2:5], v[26:29]
	s_nop 2
	s_waitcnt lgkmcnt(0)
	s_nop 3
	v_fmac_f32_e32 v244, 0x3e000000, v26
	v_cndmask_b32_e64 v96, v96, v244, s[38:39]
	s_nop 4
	v_or_b32_e32 v26, 1, v37
	v_cmp_ge_u32_e32 vcc, v26, v35
	v_cmp_lt_u32_e64 s[0:1], v26, v36
	s_and_b64 s[44:45], vcc, s[0:1]
	s_nop 2
	s_waitcnt lgkmcnt(0)
	v_fmac_f32_e32 v245, 0x3e000000, v27
	v_cndmask_b32_e64 v95, v95, v245, s[44:45]
	v_or_b32_e32 v26, 2, v37
	v_cmp_ge_u32_e32 vcc, v26, v35
	v_cmp_lt_u32_e64 s[0:1], v26, v36
	s_and_b64 s[46:47], vcc, s[0:1]
	v_mov_b32_e32 v97, 0xf149f2ca
	v_mov_b32_e32 v99, 0xf149f2ca
	s_nop 2
	s_waitcnt lgkmcnt(0)
	v_fmac_f32_e32 v246, 0x3e000000, v28
	v_cndmask_b32_e64 v99, v99, v246, s[46:47]
	v_or_b32_e32 v26, 3, v37
	v_cmp_ge_u32_e32 vcc, v26, v35
	v_cmp_lt_u32_e64 s[0:1], v26, v36
	s_and_b64 s[64:65], vcc, s[0:1]
	s_nop 2
	s_waitcnt lgkmcnt(0)
	v_fmac_f32_e32 v247, 0x3e000000, v29
	v_cndmask_b32_e64 v97, v97, v247, s[64:65]
	v_mul_u32_u24_e32 v27, 0x90, v34
	v_lshlrev_b32_e32 v26, 3, v32
	v_add_u32_e32 v32, v30, v27
	s_waitcnt vmcnt(7)
	ds_write_b128 v75, v[18:21] offset:18432
	s_waitcnt vmcnt(6)
	ds_write_b128 v75, v[22:25] offset:27648
	s_waitcnt lgkmcnt(0)
	s_barrier
; #define LAS __attribute__((address_space(3)))
; template <bool LOCAL>
; __device__ __forceinline__ void na_unit(const bf16* P, const bf16* VT, bf16* YCAT, const LAS float* rpb_l, LAS bf16* buf, int b, int gr, int hp, int qblk, int tid) {
;     ...
;     for (int sidx = 0; sidx < 2 * NCH; ++sidx) {
;         if (sidx + 2 < 2 * NCH) NA_ISSUE(sidx + 2);
;         const LAS bf16* cb = buf + (sidx & 1) * 9216 + hh * 4608;
;         if (sidx < NCH) {
;             const int c = sidx;
;             if (LOCAL && c < 8) {
; #pragma unroll
;                 for (int t2 = 0; t2 < 2; ++t2) {
;                     const LAS bf16* kp = cb + (kc0 + 16 * t2 + fr) * 72 + 8 * fq;
;                     f32x4 acc = {0.f, 0.f, 0.f, 0.f};
;                     acc = __builtin_amdgcn_mfma_f32_16x16x32_bf16(*(const LAS bf16x8*)(kp), qf[0], acc, 0, 0, 0);
;                     acc = __builtin_amdgcn_mfma_f32_16x16x32_bf16(*(const LAS bf16x8*)(kp + 32), qf[1], acc, 0, 0, 0);
;                     const LAS float* rb = rpb + (r0 + c - gr + 7) * 31 + 15 - qcol;
; #pragma unroll
;                     for (int e = 0; e < 4; ++e) { const int kcol = kc0 + 16 * t2 + 4 * fq + e; const bool ok = (kcol >= cs) && (kcol < cs + 16);
;                         const float sv = ok ? acc[e] * 0.125f + rb[ok ? kcol : qcol] : -1.0e30f; acc[e] = sv; m = fmaxf(m, sv); }
;                     sl[2 * (c < 8 ? c : 0) + t2] = acc; }
	ds_read_b32 v240, v31 offset:37916
	ds_read_b32 v241, v31 offset:37920
	ds_read_b32 v242, v31 offset:37924
	ds_read_b32 v243, v31 offset:37928
	ds_read_b32 v244, v31 offset:37980
	ds_read_b32 v245, v31 offset:37984
	ds_read_b32 v246, v31 offset:37988
	ds_read_b32 v247, v31 offset:37992
	ds_read_b128 v[18:21], v32 offset:18432
	s_add_i32 s26, s26, s15
	s_add_i32 s0, s26, 0x10c0
	v_or_b32_e32 v24, s0, v88
	v_mov_b64_e32 v[22:23], s[8:9]
	s_lshl_b32 s1, s18, 7
	v_mad_i64_i32 v[22:23], s[18:19], v24, s70, v[22:23]
	v_lshlrev_b32_e32 v70, 1, v26
	v_lshl_add_u64 v[22:23], v[22:23], 0, v[70:71]
	s_lshl_b32 s2, s1, 1
	v_lshl_add_u64 v[22:23], v[22:23], 0, s[2:3]
	ds_read_b128 v[26:29], v32 offset:18496
	s_waitcnt lgkmcnt(1)
	v_mfma_f32_16x16x32_bf16 v[34:37], v[18:21], v[6:9], 0
	v_lshl_add_u64 v[248:249], v[22:23], 0, s[100:101]
	global_load_dwordx4 v[18:21], v[22:23], off offset:1024
	s_nop 0
	global_load_dwordx4 v[22:25], v[22:23], off offset:1152
	global_load_dword v250, v[248:249], off offset:1024
	global_load_dword v251, v[248:249], off offset:1152
	v_mov_b32_e32 v98, 0xf149f2ca
	v_mov_b32_e32 v100, 0xf149f2ca
	s_waitcnt lgkmcnt(0)
	v_mfma_f32_16x16x32_bf16 v[26:29], v[26:29], v[2:5], v[34:37]
	s_nop 2
	s_waitcnt lgkmcnt(0)
	s_nop 3
	v_fmac_f32_e32 v240, 0x3e000000, v26
	v_cndmask_b32_e64 v100, v100, v240, s[28:29]
	s_nop 2
	s_waitcnt lgkmcnt(0)
	s_nop 0
	v_fmac_f32_e32 v241, 0x3e000000, v27
	v_cndmask_b32_e64 v98, v98, v241, s[30:31]
	v_mov_b32_e32 v101, 0xf149f2ca
	v_mov_b32_e32 v102, 0xf149f2ca
	s_nop 2
	s_waitcnt lgkmcnt(0)
	v_fmac_f32_e32 v242, 0x3e000000, v28
	v_cndmask_b32_e64 v102, v102, v242, s[34:35]
	s_nop 2
	s_waitcnt lgkmcnt(0)
	v_fmac_f32_e32 v243, 0x3e000000, v29
	v_cndmask_b32_e64 v101, v101, v243, s[36:37]
	v_mul_u32_u24_e32 v26, 0x90, v33
	v_add_u32_e32 v33, v30, v26
	ds_read_b128 v[26:29], v33 offset:18432
	ds_read_b128 v[34:37], v33 offset:18496
	v_mov_b32_e32 v103, 0xf149f2ca
	v_mov_b32_e32 v105, 0xf149f2ca
	s_waitcnt lgkmcnt(1)
	v_mfma_f32_16x16x32_bf16 v[26:29], v[26:29], v[6:9], 0
	s_waitcnt lgkmcnt(0)
	v_mfma_f32_16x16x32_bf16 v[26:29], v[34:37], v[2:5], v[26:29]
	s_nop 2
	s_waitcnt lgkmcnt(0)
	s_nop 3
	v_fmac_f32_e32 v244, 0x3e000000, v26
	v_cndmask_b32_e64 v105, v105, v244, s[38:39]
	s_nop 2
	s_waitcnt lgkmcnt(0)
	s_nop 0
	v_fmac_f32_e32 v245, 0x3e000000, v27
	v_cndmask_b32_e64 v103, v103, v245, s[44:45]
	v_mov_b32_e32 v107, 0xf149f2ca
	v_mov_b32_e32 v109, 0xf149f2ca
	s_nop 2
	s_waitcnt lgkmcnt(0)
	v_fmac_f32_e32 v246, 0x3e000000, v28
	v_cndmask_b32_e64 v109, v109, v246, s[46:47]
	s_nop 2
	s_waitcnt lgkmcnt(0)
	v_fmac_f32_e32 v247, 0x3e000000, v29
	v_cndmask_b32_e64 v107, v107, v247, s[64:65]
	s_waitcnt vmcnt(7)
	ds_write_b128 v75, v[10:13]
	s_waitcnt vmcnt(6)
	ds_write_b128 v75, v[14:17] offset:9216
	s_waitcnt lgkmcnt(0)
	s_barrier
	ds_read_b32 v240, v31 offset:38040
	ds_read_b32 v241, v31 offset:38044
	ds_read_b32 v242, v31 offset:38048
	ds_read_b32 v243, v31 offset:38052
	ds_read_b32 v244, v31 offset:38104
	ds_read_b32 v245, v31 offset:38108
	ds_read_b32 v246, v31 offset:38112
	ds_read_b32 v247, v31 offset:38116
	ds_read_b128 v[10:13], v32
	ds_read_b128 v[26:29], v32 offset:64
	s_add_i32 s18, s26, 0x1100
	v_or_b32_e32 v16, s18, v88
	v_mov_b64_e32 v[14:15], s[8:9]
	v_mad_i64_i32 v[14:15], s[20:21], v16, s70, v[14:15]
	v_lshl_add_u64 v[14:15], v[14:15], 0, v[70:71]
	v_lshl_add_u64 v[14:15], v[14:15], 0, s[2:3]
	s_waitcnt lgkmcnt(1)
	v_mfma_f32_16x16x32_bf16 v[34:37], v[10:13], v[6:9], 0
	v_lshl_add_u64 v[248:249], v[14:15], 0, s[100:101]
	global_load_dwordx4 v[10:13], v[14:15], off offset:1024
	s_nop 0
	global_load_dwordx4 v[14:17], v[14:15], off offset:1152
	global_load_dword v250, v[248:249], off offset:1024
	global_load_dword v251, v[248:249], off offset:1152
	v_mov_b32_e32 v104, 0xf149f2ca
	v_mov_b32_e32 v106, 0xf149f2ca
	s_waitcnt lgkmcnt(0)
	v_mfma_f32_16x16x32_bf16 v[26:29], v[26:29], v[2:5], v[34:37]
	s_nop 2
	s_waitcnt lgkmcnt(0)
	s_nop 3
	v_fmac_f32_e32 v240, 0x3e000000, v26
	v_cndmask_b32_e64 v106, v106, v240, s[28:29]
	s_nop 2
	s_waitcnt lgkmcnt(0)
	s_nop 0
	v_fmac_f32_e32 v241, 0x3e000000, v27
	v_cndmask_b32_e64 v104, v104, v241, s[30:31]
	v_mov_b32_e32 v108, 0xf149f2ca
	v_mov_b32_e32 v110, 0xf149f2ca
	s_nop 2
	s_waitcnt lgkmcnt(0)
	v_fmac_f32_e32 v242, 0x3e000000, v28
	v_cndmask_b32_e64 v110, v110, v242, s[34:35]
	s_nop 2
	s_waitcnt lgkmcnt(0)
	v_fmac_f32_e32 v243, 0x3e000000, v29
	v_cndmask_b32_e64 v108, v108, v243, s[36:37]
	ds_read_b128 v[26:29], v33
	ds_read_b128 v[34:37], v33 offset:64
	v_mov_b32_e32 v111, 0xf149f2ca
	v_mov_b32_e32 v113, 0xf149f2ca
	s_waitcnt lgkmcnt(1)
	v_mfma_f32_16x16x32_bf16 v[26:29], v[26:29], v[6:9], 0
	s_waitcnt lgkmcnt(0)
	v_mfma_f32_16x16x32_bf16 v[26:29], v[34:37], v[2:5], v[26:29]
	s_nop 2
	s_waitcnt lgkmcnt(0)
	s_nop 3
	v_fmac_f32_e32 v244, 0x3e000000, v26
	v_cndmask_b32_e64 v113, v113, v244, s[38:39]
	s_nop 2
	s_waitcnt lgkmcnt(0)
	s_nop 0
	v_fmac_f32_e32 v245, 0x3e000000, v27
	v_cndmask_b32_e64 v111, v111, v245, s[44:45]
	v_mov_b32_e32 v112, 0xf149f2ca
	v_mov_b32_e32 v116, 0xf149f2ca
	s_nop 2
	s_waitcnt lgkmcnt(0)
	v_fmac_f32_e32 v246, 0x3e000000, v28
	v_cndmask_b32_e64 v116, v116, v246, s[46:47]
	s_nop 2
	s_waitcnt lgkmcnt(0)
	v_fmac_f32_e32 v247, 0x3e000000, v29
	v_cndmask_b32_e64 v112, v112, v247, s[64:65]
	s_waitcnt vmcnt(7)
	ds_write_b128 v75, v[18:21] offset:18432
	s_waitcnt vmcnt(6)
	ds_write_b128 v75, v[22:25] offset:27648
	s_waitcnt lgkmcnt(0)
	s_barrier
; #define LAS __attribute__((address_space(3)))
; template <bool LOCAL>
; __device__ __forceinline__ void na_unit(const bf16* P, const bf16* VT, bf16* YCAT, const LAS float* rpb_l, LAS bf16* buf, int b, int gr, int hp, int qblk, int tid) {
;     ...
;     for (int sidx = 0; sidx < 2 * NCH; ++sidx) {
;         if (sidx + 2 < 2 * NCH) NA_ISSUE(sidx + 2);
;         const LAS bf16* cb = buf + (sidx & 1) * 9216 + hh * 4608;
;         if (sidx < NCH) {
;             const int c = sidx;
;             if (LOCAL && c < 8) {
; #pragma unroll
;                 for (int t2 = 0; t2 < 2; ++t2) {
;                     const LAS bf16* kp = cb + (kc0 + 16 * t2 + fr) * 72 + 8 * fq;
;                     f32x4 acc = {0.f, 0.f, 0.f, 0.f};
;                     acc = __builtin_amdgcn_mfma_f32_16x16x32_bf16(*(const LAS bf16x8*)(kp), qf[0], acc, 0, 0, 0);
;                     acc = __builtin_amdgcn_mfma_f32_16x16x32_bf16(*(const LAS bf16x8*)(kp + 32), qf[1], acc, 0, 0, 0);
;                     const LAS float* rb = rpb + (r0 + c - gr + 7) * 31 + 15 - qcol;
; #pragma unroll
;                     for (int e = 0; e < 4; ++e) { const int kcol = kc0 + 16 * t2 + 4 * fq + e; const bool ok = (kcol >= cs) && (kcol < cs + 16);
;                         const float sv = ok ? acc[e] * 0.125f + rb[ok ? kcol : qcol] : -1.0e30f; acc[e] = sv; m = fmaxf(m, sv); }
;                     sl[2 * (c < 8 ? c : 0) + t2] = acc; }
	ds_read_b32 v240, v31 offset:38164
	ds_read_b32 v241, v31 offset:38168
	ds_read_b32 v242, v31 offset:38172
	ds_read_b32 v243, v31 offset:38176
	ds_read_b32 v244, v31 offset:38228
	ds_read_b32 v245, v31 offset:38232
	ds_read_b32 v246, v31 offset:38236
	ds_read_b32 v247, v31 offset:38240
	ds_read_b128 v[18:21], v32 offset:18432
	ds_read_b128 v[26:29], v32 offset:18496
	s_add_i32 s20, s26, 0x1140
	v_or_b32_e32 v24, s20, v88
	v_mov_b64_e32 v[22:23], s[8:9]
	v_mad_i64_i32 v[22:23], s[22:23], v24, s70, v[22:23]
	v_lshl_add_u64 v[22:23], v[22:23], 0, v[70:71]
	v_lshl_add_u64 v[22:23], v[22:23], 0, s[2:3]
	s_waitcnt lgkmcnt(1)
	v_mfma_f32_16x16x32_bf16 v[34:37], v[18:21], v[6:9], 0
	v_lshl_add_u64 v[248:249], v[22:23], 0, s[100:101]
	global_load_dwordx4 v[18:21], v[22:23], off offset:1024
	s_nop 0
	global_load_dwordx4 v[22:25], v[22:23], off offset:1152
	global_load_dword v250, v[248:249], off offset:1024
	global_load_dword v251, v[248:249], off offset:1152
	v_mov_b32_e32 v114, 0xf149f2ca
	v_mov_b32_e32 v115, 0xf149f2ca
	s_waitcnt lgkmcnt(0)
	v_mfma_f32_16x16x32_bf16 v[26:29], v[26:29], v[2:5], v[34:37]
	s_nop 2
	s_waitcnt lgkmcnt(0)
	s_nop 3
	v_fmac_f32_e32 v240, 0x3e000000, v26
	v_cndmask_b32_e64 v115, v115, v240, s[28:29]
	s_nop 2
	s_waitcnt lgkmcnt(0)
	s_nop 0
	v_fmac_f32_e32 v241, 0x3e000000, v27
	v_cndmask_b32_e64 v114, v114, v241, s[30:31]
	v_mov_b32_e32 v117, 0xf149f2ca
	v_mov_b32_e32 v118, 0xf149f2ca
	s_nop 2
	s_waitcnt lgkmcnt(0)
	v_fmac_f32_e32 v242, 0x3e000000, v28
	v_cndmask_b32_e64 v118, v118, v242, s[34:35]
	s_nop 2
	s_waitcnt lgkmcnt(0)
	v_fmac_f32_e32 v243, 0x3e000000, v29
	v_cndmask_b32_e64 v117, v117, v243, s[36:37]
	ds_read_b128 v[26:29], v33 offset:18432
	ds_read_b128 v[34:37], v33 offset:18496
	v_mov_b32_e32 v119, 0xf149f2ca
	v_mov_b32_e32 v121, 0xf149f2ca
	s_waitcnt lgkmcnt(1)
	v_mfma_f32_16x16x32_bf16 v[26:29], v[26:29], v[6:9], 0
	s_waitcnt lgkmcnt(0)
	v_mfma_f32_16x16x32_bf16 v[26:29], v[34:37], v[2:5], v[26:29]
	s_nop 2
	s_waitcnt lgkmcnt(0)
	s_nop 3
	v_fmac_f32_e32 v244, 0x3e000000, v26
	v_cndmask_b32_e64 v121, v121, v244, s[38:39]
	s_nop 2
	s_waitcnt lgkmcnt(0)
	s_nop 0
	v_fmac_f32_e32 v245, 0x3e000000, v27
	v_cndmask_b32_e64 v119, v119, v245, s[44:45]
	v_mov_b32_e32 v120, 0xf149f2ca
	v_mov_b32_e32 v124, 0xf149f2ca
	s_nop 2
	s_waitcnt lgkmcnt(0)
	v_fmac_f32_e32 v246, 0x3e000000, v28
	v_cndmask_b32_e64 v124, v124, v246, s[46:47]
	s_nop 2
	s_waitcnt lgkmcnt(0)
	v_fmac_f32_e32 v247, 0x3e000000, v29
	v_cndmask_b32_e64 v120, v120, v247, s[64:65]
	s_waitcnt vmcnt(7)
	ds_write_b128 v75, v[10:13]
	s_waitcnt vmcnt(6)
	ds_write_b128 v75, v[14:17] offset:9216
	s_waitcnt lgkmcnt(0)
	s_barrier
	ds_read_b32 v240, v31 offset:38288
	ds_read_b32 v241, v31 offset:38292
	ds_read_b32 v242, v31 offset:38296
	ds_read_b32 v243, v31 offset:38300
	ds_read_b32 v244, v31 offset:38352
	ds_read_b32 v245, v31 offset:38356
	ds_read_b32 v246, v31 offset:38360
	ds_read_b32 v247, v31 offset:38364
	ds_read_b128 v[10:13], v32
	ds_read_b128 v[26:29], v32 offset:64
	s_add_i32 s22, s26, 0x1180
	v_or_b32_e32 v16, s22, v88
	v_mov_b64_e32 v[14:15], s[8:9]
	v_mad_i64_i32 v[14:15], s[24:25], v16, s70, v[14:15]
	v_lshl_add_u64 v[14:15], v[14:15], 0, v[70:71]
	v_lshl_add_u64 v[14:15], v[14:15], 0, s[2:3]
	s_waitcnt lgkmcnt(1)
	v_mfma_f32_16x16x32_bf16 v[34:37], v[10:13], v[6:9], 0
	v_lshl_add_u64 v[248:249], v[14:15], 0, s[100:101]
	global_load_dwordx4 v[10:13], v[14:15], off offset:1024
	s_nop 0
	global_load_dwordx4 v[14:17], v[14:15], off offset:1152
	global_load_dword v250, v[248:249], off offset:1024
	global_load_dword v251, v[248:249], off offset:1152
	v_mov_b32_e32 v122, 0xf149f2ca
	v_mov_b32_e32 v123, 0xf149f2ca
	s_waitcnt lgkmcnt(0)
	v_mfma_f32_16x16x32_bf16 v[26:29], v[26:29], v[2:5], v[34:37]
	s_nop 2
	s_waitcnt lgkmcnt(0)
	s_nop 3
	v_fmac_f32_e32 v240, 0x3e000000, v26
	v_cndmask_b32_e64 v123, v123, v240, s[28:29]
	s_nop 2
	s_waitcnt lgkmcnt(0)
	s_nop 0
	v_fmac_f32_e32 v241, 0x3e000000, v27
	v_cndmask_b32_e64 v122, v122, v241, s[30:31]
	v_mov_b32_e32 v125, 0xf149f2ca
	v_mov_b32_e32 v126, 0xf149f2ca
	s_nop 2
	s_waitcnt lgkmcnt(0)
	v_fmac_f32_e32 v242, 0x3e000000, v28
	v_cndmask_b32_e64 v126, v126, v242, s[34:35]
	s_nop 2
	s_waitcnt lgkmcnt(0)
	v_fmac_f32_e32 v243, 0x3e000000, v29
	v_cndmask_b32_e64 v125, v125, v243, s[36:37]
	ds_read_b128 v[26:29], v33
	ds_read_b128 v[34:37], v33 offset:64
	v_mov_b32_e32 v127, 0xf149f2ca
	v_mov_b32_e32 v129, 0xf149f2ca
	s_waitcnt lgkmcnt(1)
	v_mfma_f32_16x16x32_bf16 v[26:29], v[26:29], v[6:9], 0
	s_waitcnt lgkmcnt(0)
	v_mfma_f32_16x16x32_bf16 v[26:29], v[34:37], v[2:5], v[26:29]
	s_nop 2
	s_waitcnt lgkmcnt(0)
	s_nop 3
	v_fmac_f32_e32 v244, 0x3e000000, v26
	v_cndmask_b32_e64 v129, v129, v244, s[38:39]
	s_nop 2
	s_waitcnt lgkmcnt(0)
	s_nop 0
	v_fmac_f32_e32 v245, 0x3e000000, v27
	v_cndmask_b32_e64 v127, v127, v245, s[44:45]
	v_mov_b32_e32 v128, 0xf149f2ca
	v_mov_b32_e32 v133, 0xf149f2ca
	s_nop 2
	s_waitcnt lgkmcnt(0)
	v_fmac_f32_e32 v246, 0x3e000000, v28
	v_cndmask_b32_e64 v133, v133, v246, s[46:47]
	s_nop 2
	s_waitcnt lgkmcnt(0)
	v_fmac_f32_e32 v247, 0x3e000000, v29
	v_cndmask_b32_e64 v128, v128, v247, s[64:65]
	s_waitcnt vmcnt(7)
	ds_write_b128 v75, v[18:21] offset:18432
	s_waitcnt vmcnt(6)
	ds_write_b128 v75, v[22:25] offset:27648
	s_waitcnt lgkmcnt(0)
	s_barrier
; #define LAS __attribute__((address_space(3)))
; template <bool LOCAL>
; __device__ __forceinline__ void na_unit(const bf16* P, const bf16* VT, bf16* YCAT, const LAS float* rpb_l, LAS bf16* buf, int b, int gr, int hp, int qblk, int tid) {
;     ...
;     for (int sidx = 0; sidx < 2 * NCH; ++sidx) {
;         if (sidx + 2 < 2 * NCH) NA_ISSUE(sidx + 2);
;         const LAS bf16* cb = buf + (sidx & 1) * 9216 + hh * 4608;
;         if (sidx < NCH) {
;             const int c = sidx;
;             if (LOCAL && c < 8) {
; #pragma unroll
;                 for (int t2 = 0; t2 < 2; ++t2) {
;                     const LAS bf16* kp = cb + (kc0 + 16 * t2 + fr) * 72 + 8 * fq;
;                     f32x4 acc = {0.f, 0.f, 0.f, 0.f};
;                     acc = __builtin_amdgcn_mfma_f32_16x16x32_bf16(*(const LAS bf16x8*)(kp), qf[0], acc, 0, 0, 0);
;                     acc = __builtin_amdgcn_mfma_f32_16x16x32_bf16(*(const LAS bf16x8*)(kp + 32), qf[1], acc, 0, 0, 0);
;                     const LAS float* rb = rpb + (r0 + c - gr + 7) * 31 + 15 - qcol;
; #pragma unroll
;                     for (int e = 0; e < 4; ++e) { const int kcol = kc0 + 16 * t2 + 4 * fq + e; const bool ok = (kcol >= cs) && (kcol < cs + 16);
;                         const float sv = ok ? acc[e] * 0.125f + rb[ok ? kcol : qcol] : -1.0e30f; acc[e] = sv; m = fmaxf(m, sv); }
;                     sl[2 * (c < 8 ? c : 0) + t2] = acc; }
;             } else {
;                 const int cc = c - NLOC;
; #pragma unroll
;                 for (int t4 = 0; t4 < 4; ++t4) {
;                     const LAS bf16* kp = cb + (16 * t4 + fr) * 72 + 8 * fq;
;                     f32x4 acc = {0.f, 0.f, 0.f, 0.f};
;                     acc = __builtin_amdgcn_mfma_f32_16x16x32_bf16(*(const LAS bf16x8*)(kp), qf[0], acc, 0, 0, 0);
;                     acc = __builtin_amdgcn_mfma_f32_16x16x32_bf16(*(const LAS bf16x8*)(kp + 32), qf[1], acc, 0, 0, 0);
; #pragma unroll
;                     for (int e = 0; e < 4; ++e) { acc[e] *= 0.125f; m = fmaxf(m, acc[e]); }
;                     sc[4 * (cc >= 0 ? cc : 0) + t4] = acc; }
;             }
	ds_read_b32 v240, v31 offset:38412
	ds_read_b32 v241, v31 offset:38416
	ds_read_b32 v242, v31 offset:38420
	ds_read_b32 v243, v31 offset:38424
	ds_read_b32 v244, v31 offset:38476
	ds_read_b32 v245, v31 offset:38480
	ds_read_b32 v246, v31 offset:38484
	ds_read_b32 v247, v31 offset:38488
	ds_read_b128 v[18:21], v32 offset:18432
	ds_read_b128 v[26:29], v32 offset:18496
	s_add_i32 s24, s26, 0x11c0
	v_or_b32_e32 v24, s24, v88
	v_mov_b64_e32 v[22:23], s[8:9]
	v_mad_i64_i32 v[22:23], s[26:27], v24, s70, v[22:23]
	v_lshl_add_u64 v[22:23], v[22:23], 0, v[70:71]
	v_lshl_add_u64 v[22:23], v[22:23], 0, s[2:3]
	s_waitcnt lgkmcnt(1)
	v_mfma_f32_16x16x32_bf16 v[34:37], v[18:21], v[6:9], 0
	global_load_dwordx4 v[18:21], v[22:23], off offset:1024
	s_nop 0
	global_load_dwordx4 v[22:25], v[22:23], off offset:1152
	v_mov_b32_e32 v130, 0xf149f2ca
	v_mov_b32_e32 v131, 0xf149f2ca
	s_waitcnt lgkmcnt(0)
	v_mfma_f32_16x16x32_bf16 v[26:29], v[26:29], v[2:5], v[34:37]
	s_nop 2
	s_waitcnt lgkmcnt(0)
	s_nop 3
	v_fmac_f32_e32 v240, 0x3e000000, v26
	v_cndmask_b32_e64 v131, v131, v240, s[28:29]
	s_nop 2
	s_waitcnt lgkmcnt(0)
	s_nop 0
	v_fmac_f32_e32 v241, 0x3e000000, v27
	v_cndmask_b32_e64 v130, v130, v241, s[30:31]
	v_mov_b32_e32 v134, 0xf149f2ca
	v_mov_b32_e32 v135, 0xf149f2ca
	s_nop 2
	s_waitcnt lgkmcnt(0)
	v_fmac_f32_e32 v242, 0x3e000000, v28
	v_cndmask_b32_e64 v135, v135, v242, s[34:35]
	s_nop 2
	s_waitcnt lgkmcnt(0)
	v_fmac_f32_e32 v243, 0x3e000000, v29
	v_cndmask_b32_e64 v134, v134, v243, s[36:37]
	ds_read_b128 v[26:29], v33 offset:18432
	ds_read_b128 v[34:37], v33 offset:18496
	v_mov_b32_e32 v137, 0xf149f2ca
	v_mov_b32_e32 v139, 0xf149f2ca
	s_waitcnt lgkmcnt(1)
	v_mfma_f32_16x16x32_bf16 v[26:29], v[26:29], v[6:9], 0
	s_waitcnt lgkmcnt(0)
	v_mfma_f32_16x16x32_bf16 v[26:29], v[34:37], v[2:5], v[26:29]
	s_nop 2
	s_waitcnt lgkmcnt(0)
	s_nop 3
	v_fmac_f32_e32 v244, 0x3e000000, v26
	v_cndmask_b32_e64 v139, v139, v244, s[38:39]
	s_nop 2
	s_waitcnt lgkmcnt(0)
	s_nop 0
	v_fmac_f32_e32 v245, 0x3e000000, v27
	v_cndmask_b32_e64 v137, v137, v245, s[44:45]
	v_mov_b32_e32 v138, 0xf149f2ca
	v_mov_b32_e32 v142, 0xf149f2ca
	s_nop 2
	s_waitcnt lgkmcnt(0)
	v_fmac_f32_e32 v246, 0x3e000000, v28
	v_cndmask_b32_e64 v142, v142, v246, s[46:47]
	s_nop 2
	s_waitcnt lgkmcnt(0)
	v_fmac_f32_e32 v247, 0x3e000000, v29
	v_cndmask_b32_e64 v138, v138, v247, s[64:65]
	s_waitcnt vmcnt(5)
	ds_write_b128 v75, v[10:13]
	s_waitcnt vmcnt(4)
	ds_write_b128 v75, v[14:17] offset:9216
	s_waitcnt lgkmcnt(0)
	s_barrier
	ds_read_b32 v240, v31 offset:38536
	ds_read_b32 v241, v31 offset:38540
	ds_read_b32 v242, v31 offset:38544
	ds_read_b32 v243, v31 offset:38548
	ds_read_b32 v244, v31 offset:38600
	ds_read_b32 v245, v31 offset:38604
	ds_read_b32 v246, v31 offset:38608
	ds_read_b32 v247, v31 offset:38612
	ds_read_b128 v[10:13], v32
	ds_read_b128 v[26:29], v32 offset:64
	s_lshl_b32 s26, s17, 8
	v_or_b32_e32 v34, s26, v88
	v_mov_b64_e32 v[14:15], s[8:9]
	v_mad_i64_i32 v[14:15], s[52:53], v34, s70, v[14:15]
	v_lshl_add_u64 v[14:15], v[14:15], 0, v[70:71]
	v_lshl_add_u64 v[14:15], v[14:15], 0, s[2:3]
	s_waitcnt lgkmcnt(1)
	v_mfma_f32_16x16x32_bf16 v[36:39], v[10:13], v[6:9], 0
	v_lshl_add_u64 v[248:249], v[14:15], 0, s[100:101]
	global_load_dwordx4 v[10:13], v[14:15], off offset:1024
	s_nop 0
	global_load_dwordx4 v[14:17], v[14:15], off offset:1152
	global_load_dword v250, v[248:249], off offset:1024
	global_load_dword v251, v[248:249], off offset:1152
	v_mov_b32_e32 v140, 0xf149f2ca
	v_mov_b32_e32 v141, 0xf149f2ca
	s_waitcnt lgkmcnt(0)
	v_mfma_f32_16x16x32_bf16 v[26:29], v[26:29], v[2:5], v[36:39]
	s_nop 2
	s_waitcnt lgkmcnt(0)
	s_nop 3
	v_fmac_f32_e32 v240, 0x3e000000, v26
	v_cndmask_b32_e64 v141, v141, v240, s[28:29]
	s_nop 2
	s_waitcnt lgkmcnt(0)
	s_nop 0
	v_fmac_f32_e32 v241, 0x3e000000, v27
	v_cndmask_b32_e64 v140, v140, v241, s[30:31]
	v_mov_b32_e32 v143, 0xf149f2ca
	v_mov_b32_e32 v144, 0xf149f2ca
	s_nop 2
	s_waitcnt lgkmcnt(0)
	v_fmac_f32_e32 v242, 0x3e000000, v28
	v_cndmask_b32_e64 v144, v144, v242, s[34:35]
	s_nop 2
	s_waitcnt lgkmcnt(0)
	v_fmac_f32_e32 v243, 0x3e000000, v29
	v_cndmask_b32_e64 v143, v143, v243, s[36:37]
	ds_read_b128 v[26:29], v33
	ds_read_b128 v[36:39], v33 offset:64
	v_mov_b32_e32 v145, 0xf149f2ca
	v_mov_b32_e32 v149, 0xf149f2ca
	s_waitcnt lgkmcnt(1)
	v_mfma_f32_16x16x32_bf16 v[26:29], v[26:29], v[6:9], 0
	s_waitcnt lgkmcnt(0)
	v_mfma_f32_16x16x32_bf16 v[26:29], v[36:39], v[2:5], v[26:29]
	s_nop 2
	s_waitcnt lgkmcnt(0)
	s_nop 3
	v_fmac_f32_e32 v244, 0x3e000000, v26
	v_cndmask_b32_e64 v149, v149, v244, s[38:39]
	s_nop 2
	s_waitcnt lgkmcnt(0)
	s_nop 0
	v_fmac_f32_e32 v245, 0x3e000000, v27
	v_cndmask_b32_e64 v145, v145, v245, s[44:45]
	v_mov_b32_e32 v148, 0xf149f2ca
	v_mov_b32_e32 v152, 0xf149f2ca
	s_nop 2
	s_waitcnt lgkmcnt(0)
	v_fmac_f32_e32 v246, 0x3e000000, v28
	v_cndmask_b32_e64 v152, v152, v246, s[46:47]
	s_nop 2
	s_waitcnt lgkmcnt(0)
	v_fmac_f32_e32 v247, 0x3e000000, v29
	v_cndmask_b32_e64 v148, v148, v247, s[64:65]
	s_waitcnt vmcnt(5)
	ds_write_b128 v75, v[18:21] offset:18432
	s_waitcnt vmcnt(4)
	ds_write_b128 v75, v[22:25] offset:27648
	s_waitcnt lgkmcnt(0)
	s_barrier
; #define LAS __attribute__((address_space(3)))
; template <bool LOCAL>
; __device__ __forceinline__ void na_unit(const bf16* P, const bf16* VT, bf16* YCAT, const LAS float* rpb_l, LAS bf16* buf, int b, int gr, int hp, int qblk, int tid) {
;     ...
;     for (int sidx = 0; sidx < 2 * NCH; ++sidx) {
;         if (sidx + 2 < 2 * NCH) NA_ISSUE(sidx + 2);
;         const LAS bf16* cb = buf + (sidx & 1) * 9216 + hh * 4608;
;         if (sidx < NCH) {
;             const int c = sidx;
;             if (LOCAL && c < 8) {
; #pragma unroll
;                 for (int t2 = 0; t2 < 2; ++t2) {
;                     const LAS bf16* kp = cb + (kc0 + 16 * t2 + fr) * 72 + 8 * fq;
;                     f32x4 acc = {0.f, 0.f, 0.f, 0.f};
;                     acc = __builtin_amdgcn_mfma_f32_16x16x32_bf16(*(const LAS bf16x8*)(kp), qf[0], acc, 0, 0, 0);
;                     acc = __builtin_amdgcn_mfma_f32_16x16x32_bf16(*(const LAS bf16x8*)(kp + 32), qf[1], acc, 0, 0, 0);
;                     const LAS float* rb = rpb + (r0 + c - gr + 7) * 31 + 15 - qcol;
; #pragma unroll
;                     for (int e = 0; e < 4; ++e) { const int kcol = kc0 + 16 * t2 + 4 * fq + e; const bool ok = (kcol >= cs) && (kcol < cs + 16);
;                         const float sv = ok ? acc[e] * 0.125f + rb[ok ? kcol : qcol] : -1.0e30f; acc[e] = sv; m = fmaxf(m, sv); }
;                     sl[2 * (c < 8 ? c : 0) + t2] = acc; }
;             } else {
;                 const int cc = c - NLOC;
; #pragma unroll
;                 for (int t4 = 0; t4 < 4; ++t4) {
;                     const LAS bf16* kp = cb + (16 * t4 + fr) * 72 + 8 * fq;
;                     f32x4 acc = {0.f, 0.f, 0.f, 0.f};
;                     acc = __builtin_amdgcn_mfma_f32_16x16x32_bf16(*(const LAS bf16x8*)(kp), qf[0], acc, 0, 0, 0);
;                     acc = __builtin_amdgcn_mfma_f32_16x16x32_bf16(*(const LAS bf16x8*)(kp + 32), qf[1], acc, 0, 0, 0);
; #pragma unroll
;                     for (int e = 0; e < 4; ++e) { acc[e] *= 0.125f; m = fmaxf(m, acc[e]); }
;                     sc[4 * (cc >= 0 ? cc : 0) + t4] = acc; }
;             }
;             if (sidx == NCH - 1) { m = fmaxf(m, __shfl_xor(m, 16)); m = fmaxf(m, __shfl_xor(m, 32)); }
	ds_read_b32 v240, v31 offset:38660
	ds_read_b32 v241, v31 offset:38664
	ds_read_b32 v242, v31 offset:38668
	ds_read_b32 v243, v31 offset:38672
	ds_read_b32 v244, v31 offset:38724
	ds_read_b32 v245, v31 offset:38728
	ds_read_b32 v246, v31 offset:38732
	ds_read_b32 v247, v31 offset:38736
	ds_read_b128 v[18:21], v32 offset:18432
	ds_read_b128 v[26:29], v32 offset:18496
	v_or_b32_e32 v24, 64, v34
	v_mov_b64_e32 v[22:23], s[8:9]
	v_mad_i64_i32 v[22:23], s[52:53], v24, s70, v[22:23]
	v_lshl_add_u64 v[22:23], v[22:23], 0, v[70:71]
	v_lshl_add_u64 v[22:23], v[22:23], 0, s[2:3]
	s_waitcnt lgkmcnt(1)
	v_mfma_f32_16x16x32_bf16 v[36:39], v[18:21], v[6:9], 0
	v_lshl_add_u64 v[248:249], v[22:23], 0, s[100:101]
	global_load_dwordx4 v[18:21], v[22:23], off offset:1024
	s_nop 0
	global_load_dwordx4 v[22:25], v[22:23], off offset:1152
	global_load_dword v250, v[248:249], off offset:1024
	global_load_dword v251, v[248:249], off offset:1152
	v_mov_b32_e32 v150, 0xf149f2ca
	v_mov_b32_e32 v151, 0xf149f2ca
	s_waitcnt lgkmcnt(0)
	v_mfma_f32_16x16x32_bf16 v[26:29], v[26:29], v[2:5], v[36:39]
	s_nop 2
	s_waitcnt lgkmcnt(0)
	s_nop 3
	v_fmac_f32_e32 v240, 0x3e000000, v26
	v_cndmask_b32_e64 v151, v151, v240, s[28:29]
	s_nop 2
	s_waitcnt lgkmcnt(0)
	s_nop 0
	v_fmac_f32_e32 v241, 0x3e000000, v27
	v_cndmask_b32_e64 v150, v150, v241, s[30:31]
	v_mov_b32_e32 v153, 0xf149f2ca
	v_mov_b32_e32 v154, 0xf149f2ca
	s_nop 2
	s_waitcnt lgkmcnt(0)
	v_fmac_f32_e32 v242, 0x3e000000, v28
	v_cndmask_b32_e64 v154, v154, v242, s[34:35]
	s_nop 2
	s_waitcnt lgkmcnt(0)
	v_fmac_f32_e32 v243, 0x3e000000, v29
	v_cndmask_b32_e64 v153, v153, v243, s[36:37]
	ds_read_b128 v[26:29], v33 offset:18432
	ds_read_b128 v[36:39], v33 offset:18496
	v_mov_b32_e32 v155, 0xf149f2ca
	v_mov_b32_e32 v157, 0xf149f2ca
	s_waitcnt lgkmcnt(1)
	v_mfma_f32_16x16x32_bf16 v[26:29], v[26:29], v[6:9], 0
	s_waitcnt lgkmcnt(0)
	v_mfma_f32_16x16x32_bf16 v[26:29], v[36:39], v[2:5], v[26:29]
	s_nop 2
	s_waitcnt lgkmcnt(0)
	s_nop 3
	v_fmac_f32_e32 v244, 0x3e000000, v26
	v_cndmask_b32_e64 v157, v157, v244, s[38:39]
	s_nop 2
	s_waitcnt lgkmcnt(0)
	s_nop 0
	v_fmac_f32_e32 v245, 0x3e000000, v27
	v_cndmask_b32_e64 v155, v155, v245, s[44:45]
	v_mov_b32_e32 v156, 0xf149f2ca
	v_mov_b32_e32 v159, 0xf149f2ca
	s_nop 2
	s_waitcnt lgkmcnt(0)
	v_fmac_f32_e32 v246, 0x3e000000, v28
	v_cndmask_b32_e64 v159, v159, v246, s[46:47]
	s_nop 2
	s_waitcnt lgkmcnt(0)
	v_fmac_f32_e32 v247, 0x3e000000, v29
	v_cndmask_b32_e64 v156, v156, v247, s[64:65]
	v_max3_f32 v26, v92, s73, v91
	v_max3_f32 v26, v26, v94, v93
	v_max3_f32 v26, v26, v96, v95
	v_max3_f32 v26, v26, v99, v97
	v_max3_f32 v26, v26, v100, v98
	v_max3_f32 v26, v26, v102, v101
	v_max3_f32 v26, v26, v105, v103
	v_max3_f32 v26, v26, v109, v107
	v_max3_f32 v26, v26, v106, v104
	v_max3_f32 v26, v26, v110, v108
	v_max3_f32 v26, v26, v113, v111
	v_max3_f32 v26, v26, v116, v112
	v_max3_f32 v26, v26, v115, v114
	v_max3_f32 v26, v26, v118, v117
	v_max3_f32 v26, v26, v121, v119
	v_max3_f32 v26, v26, v124, v120
	v_max3_f32 v26, v26, v123, v122
	v_max3_f32 v26, v26, v126, v125
	v_max3_f32 v26, v26, v129, v127
	v_max3_f32 v26, v26, v133, v128
	v_max3_f32 v26, v26, v131, v130
	v_max3_f32 v26, v26, v135, v134
	v_max3_f32 v26, v26, v139, v137
	v_max3_f32 v26, v26, v142, v138
	v_max3_f32 v26, v26, v141, v140
	v_max3_f32 v26, v26, v144, v143
	v_mad_u32_u24 v89, v89, s71, v30
	v_max3_f32 v26, v26, v149, v145
	s_waitcnt vmcnt(7)
	ds_write_b128 v75, v[10:13]
	s_waitcnt vmcnt(6)
	ds_write_b128 v75, v[14:17] offset:9216
	s_waitcnt lgkmcnt(0)
	s_barrier
	ds_read_b128 v[10:13], v89
	ds_read_b128 v[14:17], v89 offset:64
	v_max3_f32 v26, v26, v152, v148
	v_max3_f32 v26, v26, v151, v150
	v_max3_f32 v26, v26, v154, v153
	v_max3_f32 v26, v26, v157, v155
	v_max3_f32 v35, v26, v159, v156
	v_or_b32_e32 v26, 0x80, v34
	v_mov_b64_e32 v[44:45], s[8:9]
	v_mad_i64_i32 v[26:27], s[28:29], v26, s70, v[44:45]
	v_lshl_add_u64 v[26:27], v[26:27], 0, v[70:71]
	v_lshl_add_u64 v[30:31], v[26:27], 0, s[2:3]
	s_waitcnt lgkmcnt(1)
	v_mfma_f32_16x16x32_bf16 v[10:13], v[10:13], v[6:9], 0
	v_lshl_add_u64 v[248:249], v[30:31], 0, s[100:101]
	global_load_dwordx4 v[26:29], v[30:31], off offset:1024
	s_nop 0
	global_load_dwordx4 v[30:33], v[30:31], off offset:1152
	global_load_dword v250, v[248:249], off offset:1024
	global_load_dword v251, v[248:249], off offset:1152
	ds_read_b128 v[36:39], v89 offset:2304
	v_lshl_add_u64 v[78:79], s[4:5], 0, v[70:71]
	s_waitcnt lgkmcnt(1)
	v_mfma_f32_16x16x32_bf16 v[62:65], v[14:17], v[2:5], v[10:13]
	s_ashr_i32 s17, s16, 31
	v_mov_b32_e32 v81, v71
	v_cmp_lt_i32_e32 vcc, v83, v84
	ds_read_b128 v[10:13], v89 offset:2368
	v_add3_u32 v158, v86, v76, v87
	s_nop 2
	v_mul_f32_e32 v14, 0x3e000000, v62
	v_mul_f32_e32 v15, 0x3e000000, v63
	v_max3_f32 v35, v35, v14, v15
	v_mul_f32_e32 v40, 0x3e000000, v64
	s_waitcnt lgkmcnt(1)
	v_mfma_f32_16x16x32_bf16 v[14:17], v[36:39], v[6:9], 0
	v_mul_f32_e32 v36, 0x3e000000, v65
	v_max3_f32 v35, v35, v40, v36
	ds_read_b128 v[36:39], v89 offset:4608
	s_waitcnt lgkmcnt(1)
	v_mfma_f32_16x16x32_bf16 v[66:69], v[10:13], v[2:5], v[14:17]
	ds_read_b128 v[10:13], v89 offset:4672
	s_ashr_i32 s19, s18, 31
	s_ashr_i32 s21, s20, 31
	s_ashr_i32 s23, s22, 31
	s_ashr_i32 s25, s24, 31
	s_nop 2
	v_mul_f32_e32 v14, 0x3e000000, v66
	v_mul_f32_e32 v15, 0x3e000000, v67
	v_max3_f32 v35, v35, v14, v15
	s_waitcnt lgkmcnt(1)
	v_mfma_f32_16x16x32_bf16 v[14:17], v[36:39], v[6:9], 0
	v_mul_f32_e32 v40, 0x3e000000, v68
	v_mul_f32_e32 v41, 0x3e000000, v69
	v_max3_f32 v35, v35, v40, v41
	s_waitcnt lgkmcnt(0)
	v_mfma_f32_16x16x32_bf16 v[58:61], v[10:13], v[2:5], v[14:17]
	ds_read_b128 v[36:39], v89 offset:6912
	ds_read_b128 v[40:43], v89 offset:6976
	s_waitcnt vmcnt(7)
	ds_write_b128 v75, v[18:21] offset:18432
	s_waitcnt vmcnt(6)
	ds_write_b128 v75, v[22:25] offset:27648
	s_waitcnt lgkmcnt(0)
	s_nop 0
	v_mul_f32_e32 v10, 0x3e000000, v58
	v_mul_f32_e32 v11, 0x3e000000, v59
	v_max3_f32 v14, v35, v10, v11
	v_mfma_f32_16x16x32_bf16 v[10:13], v[36:39], v[6:9], 0
	v_mul_f32_e32 v15, 0x3e000000, v60
	v_mul_f32_e32 v16, 0x3e000000, v61
	v_max3_f32 v14, v14, v15, v16
	v_mfma_f32_16x16x32_bf16 v[54:57], v[40:43], v[2:5], v[10:13]
	s_barrier
; #define LAS __attribute__((address_space(3)))
; template <bool LOCAL>
; __device__ __forceinline__ void na_unit(const bf16* P, const bf16* VT, bf16* YCAT, const LAS float* rpb_l, LAS bf16* buf, int b, int gr, int hp, int qblk, int tid) {
;     ...
;             } else {
;                 const int cc = c - NLOC;
; #pragma unroll
;                 for (int t4 = 0; t4 < 4; ++t4) {
;                     const LAS bf16* kp = cb + (16 * t4 + fr) * 72 + 8 * fq;
;                     f32x4 acc = {0.f, 0.f, 0.f, 0.f};
;                     acc = __builtin_amdgcn_mfma_f32_16x16x32_bf16(*(const LAS bf16x8*)(kp), qf[0], acc, 0, 0, 0);
;                     acc = __builtin_amdgcn_mfma_f32_16x16x32_bf16(*(const LAS bf16x8*)(kp + 32), qf[1], acc, 0, 0, 0);
; #pragma unroll
;                     for (int e = 0; e < 4; ++e) { acc[e] *= 0.125f; m = fmaxf(m, acc[e]); }
;                     sc[4 * (cc >= 0 ? cc : 0) + t4] = acc; }
;             }
;             if (sidx == NCH - 1) { m = fmaxf(m, __shfl_xor(m, 16)); m = fmaxf(m, __shfl_xor(m, 32)); }
	v_or_b32_e32 v18, 0xc0, v34
	v_mad_i64_i32 v[18:19], s[28:29], v18, s70, v[44:45]
	v_lshl_add_u64 v[18:19], v[18:19], 0, v[70:71]
	s_nop 3
	v_mul_f32_e32 v10, 0x3e000000, v54
	v_mul_f32_e32 v11, 0x3e000000, v55
	v_max3_f32 v14, v14, v10, v11
	ds_read_b128 v[10:13], v89 offset:18432
	v_mul_f32_e32 v15, 0x3e000000, v56
	v_mul_f32_e32 v16, 0x3e000000, v57
	v_max3_f32 v35, v14, v15, v16
	ds_read_b128 v[14:17], v89 offset:18496
	v_lshl_add_u64 v[22:23], v[18:19], 0, s[2:3]
	s_waitcnt lgkmcnt(1)
	v_mfma_f32_16x16x32_bf16 v[10:13], v[10:13], v[6:9], 0
	global_load_dwordx4 v[18:21], v[22:23], off offset:1024
	global_load_dwordx4 v[160:163], v[22:23], off offset:1152
	ds_read_b128 v[22:25], v89 offset:20736
	s_ashr_i32 s27, s26, 31
	s_waitcnt lgkmcnt(1)
	v_mfma_f32_16x16x32_bf16 v[46:49], v[14:17], v[2:5], v[10:13]
	s_nop 2
	ds_read_b128 v[10:13], v89 offset:20800
	s_nop 3
	v_mul_f32_e32 v14, 0x3e000000, v46
	v_mul_f32_e32 v15, 0x3e000000, v47
	v_max3_f32 v34, v35, v14, v15
	v_mul_f32_e32 v35, 0x3e000000, v48
	s_waitcnt lgkmcnt(1)
	v_mfma_f32_16x16x32_bf16 v[14:17], v[22:25], v[6:9], 0
	v_mul_f32_e32 v22, 0x3e000000, v49
	v_max3_f32 v34, v34, v35, v22
	ds_read_b128 v[22:25], v89 offset:23040
	s_waitcnt lgkmcnt(1)
	v_mfma_f32_16x16x32_bf16 v[50:53], v[10:13], v[2:5], v[14:17]
	ds_read_b128 v[10:13], v89 offset:23104
	s_nop 6
	v_mul_f32_e32 v14, 0x3e000000, v50
	v_mul_f32_e32 v15, 0x3e000000, v51
	v_max3_f32 v34, v34, v14, v15
	s_waitcnt lgkmcnt(1)
	v_mfma_f32_16x16x32_bf16 v[14:17], v[22:25], v[6:9], 0
	v_mul_f32_e32 v35, 0x3e000000, v52
	v_mul_f32_e32 v36, 0x3e000000, v53
	v_max3_f32 v38, v34, v35, v36
	s_waitcnt lgkmcnt(0)
	v_mfma_f32_16x16x32_bf16 v[42:45], v[10:13], v[2:5], v[14:17]
	ds_read_b128 v[22:25], v89 offset:25344
	ds_read_b128 v[34:37], v89 offset:25408
	s_waitcnt vmcnt(5)
	ds_write_b128 v75, v[26:29]
	s_waitcnt vmcnt(4)
	ds_write_b128 v75, v[30:33] offset:9216
	s_waitcnt lgkmcnt(0)
	s_nop 0
	v_mul_f32_e32 v10, 0x3e000000, v42
	v_mul_f32_e32 v11, 0x3e000000, v43
	v_max3_f32 v14, v38, v10, v11
	v_mfma_f32_16x16x32_bf16 v[10:13], v[22:25], v[6:9], 0
	v_mul_f32_e32 v15, 0x3e000000, v44
	v_mul_f32_e32 v16, 0x3e000000, v45
	v_max3_f32 v14, v14, v15, v16
	v_mfma_f32_16x16x32_bf16 v[38:41], v[34:37], v[2:5], v[10:13]
	s_barrier
	v_add3_u32 v26, v88, s1, 64
	v_mul_u32_u24_e32 v26, 0x9000, v26
	v_lshl_add_u64 v[22:23], s[16:17], 1, v[78:79]
	s_nop 3
	v_mul_f32_e32 v10, 0x3e000000, v38
	v_mul_f32_e32 v11, 0x3e000000, v39
	v_max3_f32 v10, v14, v10, v11
	v_mul_f32_e32 v11, 0x3e000000, v40
	v_mul_f32_e32 v12, 0x3e000000, v41
	v_max3_f32 v34, v10, v11, v12
	v_or_b32_e32 v10, s1, v88
	v_mul_u32_u24_e32 v14, 0x9000, v10
	ds_read_b128 v[10:13], v89
	v_lshlrev_b32_e32 v70, 1, v14
	ds_read_b128 v[14:17], v89 offset:64
	v_lshlrev_b32_e32 v80, 1, v26
	v_lshl_add_u64 v[24:25], v[22:23], 0, v[70:71]
	v_lshl_add_u64 v[22:23], v[22:23], 0, v[80:81]
	s_waitcnt lgkmcnt(1)
	v_mfma_f32_16x16x32_bf16 v[10:13], v[10:13], v[6:9], 0
	v_lshl_add_u64 v[248:249], v[24:25], 0, 0
	v_lshl_add_u64 v[238:239], v[22:23], 0, 0
	global_load_dwordx4 v[164:167], v[24:25], off
	global_load_dwordx4 v[168:171], v[22:23], off
	global_load_dword v250, v[248:249], off offset:128
	global_load_dword v251, v[238:239], off offset:128
	ds_read_b128 v[22:25], v89 offset:2304
	s_add_i32 s16, s15, s50
	s_waitcnt lgkmcnt(1)
	v_mfma_f32_16x16x32_bf16 v[30:33], v[14:17], v[2:5], v[10:13]
	s_ashr_i32 s17, s16, 31
	s_ashr_i32 s15, s14, 31
	v_lshl_add_u64 v[86:87], s[14:15], 1, v[78:79]
	ds_read_b128 v[10:13], v89 offset:2368
	s_ashr_i32 s1, s0, 31
	s_nop 2
	v_mul_f32_e32 v14, 0x3e000000, v30
	v_mul_f32_e32 v15, 0x3e000000, v31
	v_max3_f32 v26, v34, v14, v15
	v_mul_f32_e32 v27, 0x3e000000, v32
	s_waitcnt lgkmcnt(1)
	v_mfma_f32_16x16x32_bf16 v[14:17], v[22:25], v[6:9], 0
	v_mul_f32_e32 v22, 0x3e000000, v33
	v_max3_f32 v26, v26, v27, v22
	ds_read_b128 v[22:25], v89 offset:4608
	s_waitcnt lgkmcnt(1)
	v_mfma_f32_16x16x32_bf16 v[34:37], v[10:13], v[2:5], v[14:17]
	ds_read_b128 v[10:13], v89 offset:4672
	s_nop 6
	v_mul_f32_e32 v14, 0x3e000000, v34
	v_mul_f32_e32 v15, 0x3e000000, v35
	v_max3_f32 v26, v26, v14, v15
	s_waitcnt lgkmcnt(1)
	v_mfma_f32_16x16x32_bf16 v[14:17], v[22:25], v[6:9], 0
	v_mul_f32_e32 v27, 0x3e000000, v36
	v_mul_f32_e32 v28, 0x3e000000, v37
	v_max3_f32 v88, v26, v27, v28
	s_waitcnt lgkmcnt(0)
	v_mfma_f32_16x16x32_bf16 v[26:29], v[10:13], v[2:5], v[14:17]
	ds_read_b128 v[22:25], v89 offset:6912
	ds_read_b128 v[172:175], v89 offset:6976
	s_waitcnt vmcnt(5)
	ds_write_b128 v75, v[18:21] offset:18432
	s_waitcnt vmcnt(4)
	ds_write_b128 v75, v[160:163] offset:27648
	s_waitcnt lgkmcnt(0)
	s_nop 0
	v_mul_f32_e32 v10, 0x3e000000, v26
	v_mul_f32_e32 v11, 0x3e000000, v27
	v_max3_f32 v14, v88, v10, v11
	v_mfma_f32_16x16x32_bf16 v[10:13], v[22:25], v[6:9], 0
	v_mul_f32_e32 v15, 0x3e000000, v28
	v_mul_f32_e32 v16, 0x3e000000, v29
	v_max3_f32 v14, v14, v15, v16
	v_mfma_f32_16x16x32_bf16 v[22:25], v[172:175], v[2:5], v[10:13]
	s_barrier
; #define LAS __attribute__((address_space(3)))
; __device__ __forceinline__ unsigned cvt_pk_bf16(float lo, float hi) { const float __attribute__((ext_vector_type(2))) v = {lo, hi}; return __builtin_bit_cast(unsigned, __builtin_convertvector(v, bf16x2_t)); }
; template <bool LOCAL>
; __device__ __forceinline__ void na_unit(const bf16* P, const bf16* VT, bf16* YCAT, const LAS float* rpb_l, LAS bf16* buf, int b, int gr, int hp, int qblk, int tid) {
;     ...
;             if (sidx == NCH - 1) { m = fmaxf(m, __shfl_xor(m, 16)); m = fmaxf(m, __shfl_xor(m, 32)); }
;         } else {
;             const int c = sidx - NCH;
;             if (LOCAL && c < 8) {
;                 float p[8];
; #pragma unroll
;                 for (int e = 0; e < 4; ++e) { p[e] = __expf(sl[2 * (c < 8 ? c : 0)][e] - m); p[4 + e] = __expf(sl[2 * (c < 8 ? c : 0) + 1][e] - m); }
; #pragma unroll
;                 for (int e = 0; e < 8; ++e) lsum += p[e];
;                 const bf16x8 pf = __builtin_bit_cast(bf16x8, (v4u){pg8::cvt_pk_bf16(p[0], p[1]), pg8::cvt_pk_bf16(p[2], p[3]), pg8::cvt_pk_bf16(p[4], p[5]), pg8::cvt_pk_bf16(p[6], p[7])});
; #pragma unroll
;                 for (int dt = 0; dt < 4; ++dt) { const LAS bf16* vp = cb + (16 * dt + fr) * 72 + kc0 + 4 * fq;
;                     o[dt] = __builtin_amdgcn_mfma_f32_16x16x32_bf16(frag44(vp, vp + 16), pf, o[dt], 0, 0, 0); }
	v_lshl_add_u64 v[18:19], s[16:17], 1, v[78:79]
	v_lshl_add_u64 v[20:21], v[18:19], 0, v[70:71]
	v_lshl_add_u64 v[18:19], v[18:19], 0, v[80:81]
	s_nop 3
	v_mul_f32_e32 v10, 0x3e000000, v22
	v_mul_f32_e32 v11, 0x3e000000, v23
	v_max3_f32 v14, v14, v10, v11
	ds_read_b128 v[10:13], v89 offset:18432
	v_mul_f32_e32 v15, 0x3e000000, v24
	v_mul_f32_e32 v16, 0x3e000000, v25
	v_max3_f32 v88, v14, v15, v16
	ds_read_b128 v[14:17], v89 offset:18496
	s_waitcnt lgkmcnt(1)
	v_mfma_f32_16x16x32_bf16 v[10:13], v[10:13], v[6:9], 0
	v_lshl_add_u64 v[248:249], v[20:21], 0, 0
	v_lshl_add_u64 v[238:239], v[18:19], 0, 0
	global_load_dwordx4 v[172:175], v[20:21], off
	global_load_dwordx4 v[176:179], v[18:19], off
	global_load_dword v250, v[248:249], off offset:128
	global_load_dword v251, v[238:239], off offset:128
	ds_read_b128 v[18:21], v89 offset:20736
	ds_read_b128 v[160:163], v89 offset:23040
	s_waitcnt lgkmcnt(2)
	v_mfma_f32_16x16x32_bf16 v[14:17], v[14:17], v[2:5], v[10:13]
	s_nop 2
	ds_read_b128 v[10:13], v89 offset:20800
	s_waitcnt lgkmcnt(2)
	v_mfma_f32_16x16x32_bf16 v[18:21], v[18:21], v[6:9], 0
	s_nop 1
	v_mul_f32_e32 v132, 0x3e000000, v14
	v_mul_f32_e32 v136, 0x3e000000, v15
	v_max3_f32 v88, v88, v132, v136
	s_waitcnt lgkmcnt(0)
	v_mfma_f32_16x16x32_bf16 v[18:21], v[10:13], v[2:5], v[18:21]
	ds_read_b128 v[10:13], v89 offset:23104
	ds_read_b128 v[180:183], v89 offset:25344
	ds_read_b128 v[184:187], v89 offset:25408
	v_mul_f32_e32 v132, 0x3e000000, v16
	v_mfma_f32_16x16x32_bf16 v[160:163], v[160:163], v[6:9], 0
	v_mul_f32_e32 v136, 0x3e000000, v17
	v_max3_f32 v88, v88, v132, v136
	s_nop 0
	v_mul_f32_e32 v132, 0x3e000000, v18
	s_waitcnt lgkmcnt(1)
	v_mfma_f32_16x16x32_bf16 v[6:9], v[180:183], v[6:9], 0
	v_mul_f32_e32 v136, 0x3e000000, v19
	v_max3_f32 v88, v88, v132, v136
	v_mul_f32_e32 v132, 0x3e000000, v20
	v_mfma_f32_16x16x32_bf16 v[10:13], v[10:13], v[2:5], v[160:163]
	v_mul_f32_e32 v136, 0x3e000000, v21
	v_max3_f32 v88, v88, v132, v136
	s_waitcnt vmcnt(7)
	ds_write_b128 v75, v[164:167]
	s_waitcnt vmcnt(6)
	ds_write_b128 v75, v[168:171] offset:9216
	s_waitcnt lgkmcnt(2)
	v_mfma_f32_16x16x32_bf16 v[2:5], v[184:187], v[2:5], v[6:9]
	v_mul_f32_e32 v89, 0x3e000000, v10
	v_mul_f32_e32 v132, 0x3e000000, v11
	v_max3_f32 v88, v88, v89, v132
	v_mul_f32_e32 v89, 0x3e000000, v12
	v_mul_f32_e32 v132, 0x3e000000, v13
	v_max3_f32 v88, v88, v89, v132
	s_nop 1
	v_mul_f32_e32 v6, 0x3e000000, v2
	v_mul_f32_e32 v7, 0x3e000000, v3
	v_max3_f32 v6, v88, v6, v7
	v_mul_f32_e32 v7, 0x3e000000, v4
	v_mul_f32_e32 v8, 0x3e000000, v5
	v_max3_f32 v6, v6, v7, v8
	v_cndmask_b32_e32 v7, v82, v83, vcc
	v_lshlrev_b32_e32 v88, 2, v7
	ds_bpermute_b32 v7, v88, v6
	v_cmp_lt_i32_e32 vcc, v85, v84
	v_lshl_add_u32 v8, v90, 1, v158
	s_waitcnt lgkmcnt(0)
	s_barrier
	v_max_f32_e32 v7, v7, v7
	v_max_f32_e32 v6, v6, v7
	v_cndmask_b32_e32 v7, v82, v85, vcc
	v_lshlrev_b32_e32 v89, 2, v7
	ds_bpermute_b32 v7, v89, v6
	s_waitcnt lgkmcnt(0)
	ds_read2_b64 v[160:163], v8 offset1:4
	v_max_f32_e32 v7, v7, v7
	v_max_f32_e32 v136, v6, v7
	v_sub_f32_e32 v6, v92, v136
	v_mul_f32_e32 v6, 0x3fb8aa3b, v6
	v_exp_f32_e32 v132, v6
	v_sub_f32_e32 v6, v96, v136
	v_mul_f32_e32 v6, 0x3fb8aa3b, v6
	v_exp_f32_e32 v92, v6
	v_sub_f32_e32 v6, v91, v136
	v_mul_f32_e32 v6, 0x3fb8aa3b, v6
	v_exp_f32_e32 v96, v6
	v_sub_f32_e32 v6, v95, v136
	v_mul_f32_e32 v6, 0x3fb8aa3b, v6
	v_exp_f32_e32 v91, v6
	v_sub_f32_e32 v6, v94, v136
	v_mul_f32_e32 v6, 0x3fb8aa3b, v6
	v_exp_f32_e32 v95, v6
	v_sub_f32_e32 v6, v99, v136
	v_mul_f32_e32 v6, 0x3fb8aa3b, v6
	v_exp_f32_e32 v94, v6
	v_sub_f32_e32 v6, v93, v136
	v_mul_f32_e32 v6, 0x3fb8aa3b, v6
	v_exp_f32_e32 v99, v6
	v_sub_f32_e32 v6, v97, v136
	v_mul_f32_e32 v6, 0x3fb8aa3b, v6
	v_exp_f32_e32 v93, v6
	v_cvt_pk_bf16_f32 v164, v132, v96
	v_cvt_pk_bf16_f32 v165, v95, v99
	v_cvt_pk_bf16_f32 v166, v92, v91
	v_cvt_pk_bf16_f32 v167, v94, v93
	v_add_u32_e32 v7, 0x800, v8
	v_add_u32_e32 v6, 0x1000, v8
	s_waitcnt lgkmcnt(0)
	v_mfma_f32_16x16x32_bf16 v[184:187], v[160:163], v[164:167], 0
	v_lshl_add_u64 v[160:161], v[86:87], 0, v[70:71]
	ds_read2_b64 v[168:171], v7 offset0:32 offset1:36
	ds_read2_b64 v[180:183], v6 offset0:64 offset1:68
	v_lshl_add_u64 v[86:87], v[86:87], 0, v[80:81]
	v_lshl_add_u64 v[248:249], v[160:161], 0, 0
	v_lshl_add_u64 v[238:239], v[86:87], 0, 0
	global_load_dwordx4 v[188:191], v[160:161], off
	global_load_dwordx4 v[192:195], v[86:87], off
	global_load_dword v250, v[248:249], off offset:128
	global_load_dword v251, v[238:239], off offset:128
	v_sub_f32_e32 v9, v100, v136
	v_mul_f32_e32 v9, 0x3fb8aa3b, v9
	v_add_u32_e32 v160, 0x1800, v8
	v_exp_f32_e32 v86, v9
	v_sub_f32_e32 v9, v105, v136
	ds_read2_b64 v[196:199], v160 offset0:96 offset1:100
	v_mul_f32_e32 v9, 0x3fb8aa3b, v9
	v_exp_f32_e32 v76, v9
	v_sub_f32_e32 v9, v98, v136
	v_mul_f32_e32 v9, 0x3fb8aa3b, v9
	v_exp_f32_e32 v90, v9
	v_sub_f32_e32 v9, v103, v136
	v_mul_f32_e32 v9, 0x3fb8aa3b, v9
	v_exp_f32_e32 v87, v9
	v_sub_f32_e32 v9, v102, v136
	v_mul_f32_e32 v9, 0x3fb8aa3b, v9
	v_exp_f32_e32 v98, v9
	v_sub_f32_e32 v9, v109, v136
	v_mul_f32_e32 v9, 0x3fb8aa3b, v9
	v_add_u32_e32 v162, 0x4800, v8
	s_waitcnt lgkmcnt(2)
	v_mfma_f32_16x16x32_bf16 v[168:171], v[168:171], v[164:167], 0
	s_waitcnt vmcnt(7)
	ds_write_b128 v75, v[172:175] offset:18432
	s_waitcnt vmcnt(6)
	ds_write_b128 v75, v[176:179] offset:27648
	s_waitcnt lgkmcnt(0)
	s_barrier
; #define LAS __attribute__((address_space(3)))
; __device__ __forceinline__ unsigned cvt_pk_bf16(float lo, float hi) { const float __attribute__((ext_vector_type(2))) v = {lo, hi}; return __builtin_bit_cast(unsigned, __builtin_convertvector(v, bf16x2_t)); }
; template <bool LOCAL>
; __device__ __forceinline__ void na_unit(const bf16* P, const bf16* VT, bf16* YCAT, const LAS float* rpb_l, LAS bf16* buf, int b, int gr, int hp, int qblk, int tid) {
;     ...
;             const int c = sidx - NCH;
;             if (LOCAL && c < 8) {
;                 float p[8];
; #pragma unroll
;                 for (int e = 0; e < 4; ++e) { p[e] = __expf(sl[2 * (c < 8 ? c : 0)][e] - m); p[4 + e] = __expf(sl[2 * (c < 8 ? c : 0) + 1][e] - m); }
; #pragma unroll
;                 for (int e = 0; e < 8; ++e) lsum += p[e];
;                 const bf16x8 pf = __builtin_bit_cast(bf16x8, (v4u){pg8::cvt_pk_bf16(p[0], p[1]), pg8::cvt_pk_bf16(p[2], p[3]), pg8::cvt_pk_bf16(p[4], p[5]), pg8::cvt_pk_bf16(p[6], p[7])});
; #pragma unroll
;                 for (int dt = 0; dt < 4; ++dt) { const LAS bf16* vp = cb + (16 * dt + fr) * 72 + kc0 + 4 * fq;
;                     o[dt] = __builtin_amdgcn_mfma_f32_16x16x32_bf16(frag44(vp, vp + 16), pf, o[dt], 0, 0, 0); }
	v_mfma_f32_16x16x32_bf16 v[180:183], v[180:183], v[164:167], 0
	v_exp_f32_e32 v97, v9
	v_sub_f32_e32 v9, v101, v136
	v_mfma_f32_16x16x32_bf16 v[196:199], v[196:199], v[164:167], 0
	ds_read2_b64 v[164:167], v162 offset1:4
	v_add_u32_e32 v161, 0x5000, v8
	v_mul_f32_e32 v9, 0x3fb8aa3b, v9
	ds_read2_b64 v[172:175], v161 offset0:32 offset1:36
	v_exp_f32_e32 v100, v9
	v_sub_f32_e32 v9, v107, v136
	v_mul_f32_e32 v9, 0x3fb8aa3b, v9
	v_exp_f32_e32 v101, v9
	v_cvt_pk_bf16_f32 v176, v86, v90
	v_cvt_pk_bf16_f32 v177, v98, v100
	v_cvt_pk_bf16_f32 v178, v76, v87
	v_cvt_pk_bf16_f32 v179, v97, v101
	v_lshl_add_u64 v[102:103], s[0:1], 1, v[78:79]
	v_add_u32_e32 v163, 0x5800, v8
	s_waitcnt lgkmcnt(1)
	v_mfma_f32_16x16x32_bf16 v[184:187], v[164:167], v[176:179], v[184:187]
	v_lshl_add_u64 v[164:165], v[102:103], 0, v[70:71]
	v_lshl_add_u64 v[102:103], v[102:103], 0, v[80:81]
	v_sub_f32_e32 v9, v106, v136
	s_waitcnt lgkmcnt(0)
	v_mfma_f32_16x16x32_bf16 v[166:169], v[172:175], v[176:179], v[168:171]
	v_mul_f32_e32 v9, 0x3fb8aa3b, v9
	v_fma_f32 v62, v62, s72, -v136
	v_fma_f32 v63, v63, s72, -v136
	ds_read2_b64 v[170:173], v163 offset0:64 offset1:68
	v_lshl_add_u64 v[248:249], v[164:165], 0, 0
	v_lshl_add_u64 v[238:239], v[102:103], 0, 0
	global_load_dwordx4 v[200:203], v[164:165], off
	global_load_dwordx4 v[204:207], v[102:103], off
	global_load_dword v250, v[248:249], off offset:128
	global_load_dword v251, v[238:239], off offset:128
	v_add_u32_e32 v164, 0x6000, v8
	v_exp_f32_e32 v103, v9
	v_sub_f32_e32 v9, v113, v136
	s_waitcnt lgkmcnt(0)
	v_mfma_f32_16x16x32_bf16 v[170:173], v[170:173], v[176:179], v[180:183]
	s_nop 2
	ds_read2_b64 v[180:183], v164 offset0:96 offset1:100
	v_mul_f32_e32 v9, 0x3fb8aa3b, v9
	v_exp_f32_e32 v102, v9
	v_sub_f32_e32 v9, v104, v136
	v_mul_f32_e32 v9, 0x3fb8aa3b, v9
	v_exp_f32_e32 v105, v9
	v_sub_f32_e32 v9, v111, v136
	v_mul_f32_e32 v9, 0x3fb8aa3b, v9
	v_exp_f32_e32 v104, v9
	v_sub_f32_e32 v9, v110, v136
	v_mul_f32_e32 v9, 0x3fb8aa3b, v9
	v_exp_f32_e32 v107, v9
	v_sub_f32_e32 v9, v116, v136
	v_mul_f32_e32 v9, 0x3fb8aa3b, v9
	s_waitcnt lgkmcnt(0)
	v_mfma_f32_16x16x32_bf16 v[174:177], v[180:183], v[176:179], v[196:199]
	s_waitcnt vmcnt(7)
	ds_write_b128 v75, v[188:191]
	s_waitcnt vmcnt(6)
	ds_write_b128 v75, v[192:195] offset:9216
	s_waitcnt lgkmcnt(0)
	s_barrier
	v_exp_f32_e32 v106, v9
	v_sub_f32_e32 v9, v108, v136
	ds_read2_b64 v[178:181], v8 offset1:4
	v_mul_f32_e32 v9, 0x3fb8aa3b, v9
	v_exp_f32_e32 v108, v9
	v_sub_f32_e32 v9, v112, v136
	v_mul_f32_e32 v9, 0x3fb8aa3b, v9
	v_exp_f32_e32 v109, v9
	v_lshl_add_u64 v[192:193], s[18:19], 1, v[78:79]
	v_cvt_pk_bf16_f32 v188, v103, v105
	v_cvt_pk_bf16_f32 v189, v107, v108
	v_cvt_pk_bf16_f32 v190, v102, v104
	v_cvt_pk_bf16_f32 v191, v106, v109
	v_lshl_add_u64 v[196:197], v[192:193], 0, v[80:81]
	ds_read2_b64 v[110:113], v7 offset0:32 offset1:36
	s_waitcnt lgkmcnt(1)
	v_mfma_f32_16x16x32_bf16 v[178:181], v[178:181], v[188:191], v[184:187]
	v_sub_f32_e32 v9, v115, v136
	v_mul_f32_e32 v9, 0x3fb8aa3b, v9
	v_fma_f32 v64, v64, s72, -v136
	v_lshl_add_u64 v[186:187], v[192:193], 0, v[70:71]
	ds_read2_b64 v[182:185], v6 offset0:64 offset1:68
	v_lshl_add_u64 v[248:249], v[186:187], 0, 0
	v_lshl_add_u64 v[238:239], v[196:197], 0, 0
	global_load_dwordx4 v[192:195], v[186:187], off
	s_nop 0
	global_load_dwordx4 v[196:199], v[196:197], off
	global_load_dword v250, v[248:249], off offset:128
	global_load_dword v251, v[238:239], off offset:128
	s_waitcnt lgkmcnt(1)
	v_mfma_f32_16x16x32_bf16 v[166:169], v[110:113], v[188:191], v[166:169]
	ds_read2_b64 v[110:113], v160 offset0:96 offset1:100
	s_waitcnt vmcnt(7)
	ds_write_b128 v75, v[200:203] offset:18432
	s_waitcnt vmcnt(6)
	ds_write_b128 v75, v[204:207] offset:27648
	s_waitcnt lgkmcnt(2)
	v_mfma_f32_16x16x32_bf16 v[174:177], v[110:113], v[188:191], v[174:177]
	v_exp_f32_e32 v111, v9
	v_sub_f32_e32 v9, v121, v136
	v_mul_f32_e32 v9, 0x3fb8aa3b, v9
	v_exp_f32_e32 v110, v9
	v_sub_f32_e32 v9, v114, v136
	v_mul_f32_e32 v9, 0x3fb8aa3b, v9
	v_exp_f32_e32 v113, v9
	v_sub_f32_e32 v9, v119, v136
	v_mul_f32_e32 v9, 0x3fb8aa3b, v9
	v_exp_f32_e32 v112, v9
	v_sub_f32_e32 v9, v118, v136
	v_mul_f32_e32 v9, 0x3fb8aa3b, v9
	v_exp_f32_e32 v115, v9
	v_sub_f32_e32 v9, v124, v136
	v_mul_f32_e32 v9, 0x3fb8aa3b, v9
	v_exp_f32_e32 v114, v9
	v_sub_f32_e32 v9, v117, v136
	v_mul_f32_e32 v9, 0x3fb8aa3b, v9
	v_mfma_f32_16x16x32_bf16 v[170:173], v[182:185], v[188:191], v[170:173]
	s_waitcnt lgkmcnt(0)
	s_barrier
	v_exp_f32_e32 v116, v9
	ds_read2_b64 v[182:185], v162 offset1:4
	v_sub_f32_e32 v9, v120, v136
	ds_read2_b64 v[118:121], v161 offset0:32 offset1:36
	v_mul_f32_e32 v9, 0x3fb8aa3b, v9
	v_exp_f32_e32 v117, v9
	v_lshl_add_u64 v[190:191], s[20:21], 1, v[78:79]
	v_lshl_add_u64 v[200:201], v[190:191], 0, v[70:71]
	v_cvt_pk_bf16_f32 v186, v111, v113
	v_cvt_pk_bf16_f32 v187, v115, v116
	v_cvt_pk_bf16_f32 v188, v110, v112
	v_cvt_pk_bf16_f32 v189, v114, v117
	v_lshl_add_u64 v[190:191], v[190:191], 0, v[80:81]
	v_sub_f32_e32 v9, v123, v136
	s_waitcnt lgkmcnt(1)
	v_mfma_f32_16x16x32_bf16 v[178:181], v[182:185], v[186:189], v[178:181]
	v_lshl_add_u64 v[248:249], v[200:201], 0, 0
	v_lshl_add_u64 v[238:239], v[190:191], 0, 0
	global_load_dwordx4 v[182:185], v[200:201], off
	s_nop 0
	global_load_dwordx4 v[200:203], v[190:191], off
	global_load_dword v250, v[248:249], off offset:128
	global_load_dword v251, v[238:239], off offset:128
	v_mul_f32_e32 v9, 0x3fb8aa3b, v9
	v_fma_f32 v65, v65, s72, -v136
	s_waitcnt lgkmcnt(0)
	v_mfma_f32_16x16x32_bf16 v[166:169], v[118:121], v[186:189], v[166:169]
	ds_read2_b64 v[118:121], v163 offset0:64 offset1:68
	v_mul_f32_e32 v62, 0x3fb8aa3b, v62
	v_mul_f32_e32 v63, 0x3fb8aa3b, v63
	s_waitcnt lgkmcnt(0)
	v_mfma_f32_16x16x32_bf16 v[170:173], v[118:121], v[186:189], v[170:173]
	ds_read2_b64 v[118:121], v164 offset0:96 offset1:100
	s_waitcnt vmcnt(7)
	ds_write_b128 v75, v[192:195]
	s_waitcnt vmcnt(6)
	ds_write_b128 v75, v[196:199] offset:9216
	s_waitcnt lgkmcnt(0)
	v_mfma_f32_16x16x32_bf16 v[174:177], v[118:121], v[186:189], v[174:177]
	v_exp_f32_e32 v119, v9
	v_sub_f32_e32 v9, v129, v136
	v_mul_f32_e32 v9, 0x3fb8aa3b, v9
	v_exp_f32_e32 v118, v9
	v_sub_f32_e32 v9, v122, v136
	v_mul_f32_e32 v9, 0x3fb8aa3b, v9
	v_exp_f32_e32 v121, v9
	v_sub_f32_e32 v9, v127, v136
	v_mul_f32_e32 v9, 0x3fb8aa3b, v9
	v_exp_f32_e32 v120, v9
	v_sub_f32_e32 v9, v126, v136
	v_mul_f32_e32 v9, 0x3fb8aa3b, v9
	v_exp_f32_e32 v123, v9
	v_sub_f32_e32 v9, v133, v136
	v_mul_f32_e32 v9, 0x3fb8aa3b, v9
	s_barrier
; #define LAS __attribute__((address_space(3)))
; __device__ __forceinline__ unsigned cvt_pk_bf16(float lo, float hi) { const float __attribute__((ext_vector_type(2))) v = {lo, hi}; return __builtin_bit_cast(unsigned, __builtin_convertvector(v, bf16x2_t)); }
; template <bool LOCAL>
; __device__ __forceinline__ void na_unit(const bf16* P, const bf16* VT, bf16* YCAT, const LAS float* rpb_l, LAS bf16* buf, int b, int gr, int hp, int qblk, int tid) {
;     ...
;             const int c = sidx - NCH;
;             if (LOCAL && c < 8) {
;                 float p[8];
; #pragma unroll
;                 for (int e = 0; e < 4; ++e) { p[e] = __expf(sl[2 * (c < 8 ? c : 0)][e] - m); p[4 + e] = __expf(sl[2 * (c < 8 ? c : 0) + 1][e] - m); }
; #pragma unroll
;                 for (int e = 0; e < 8; ++e) lsum += p[e];
;                 const bf16x8 pf = __builtin_bit_cast(bf16x8, (v4u){pg8::cvt_pk_bf16(p[0], p[1]), pg8::cvt_pk_bf16(p[2], p[3]), pg8::cvt_pk_bf16(p[4], p[5]), pg8::cvt_pk_bf16(p[6], p[7])});
; #pragma unroll
;                 for (int dt = 0; dt < 4; ++dt) { const LAS bf16* vp = cb + (16 * dt + fr) * 72 + kc0 + 4 * fq;
;                     o[dt] = __builtin_amdgcn_mfma_f32_16x16x32_bf16(frag44(vp, vp + 16), pf, o[dt], 0, 0, 0); }
	v_exp_f32_e32 v122, v9
	v_sub_f32_e32 v9, v125, v136
	ds_read2_b64 v[186:189], v8 offset1:4
	v_mul_f32_e32 v9, 0x3fb8aa3b, v9
	v_exp_f32_e32 v124, v9
	v_sub_f32_e32 v9, v128, v136
	v_mul_f32_e32 v9, 0x3fb8aa3b, v9
	v_exp_f32_e32 v125, v9
	v_lshl_add_u64 v[194:195], s[22:23], 1, v[78:79]
	v_cvt_pk_bf16_f32 v190, v119, v121
	v_cvt_pk_bf16_f32 v191, v123, v124
	v_cvt_pk_bf16_f32 v192, v118, v120
	v_cvt_pk_bf16_f32 v193, v122, v125
	v_lshl_add_u64 v[196:197], v[194:195], 0, v[70:71]
	ds_read2_b64 v[126:129], v7 offset0:32 offset1:36
	s_waitcnt lgkmcnt(1)
	v_mfma_f32_16x16x32_bf16 v[178:181], v[186:189], v[190:193], v[178:181]
	ds_read2_b64 v[186:189], v6 offset0:64 offset1:68
	v_lshl_add_u64 v[198:199], v[194:195], 0, v[80:81]
	v_lshl_add_u64 v[248:249], v[196:197], 0, 0
	v_lshl_add_u64 v[238:239], v[198:199], 0, 0
	global_load_dwordx4 v[194:197], v[196:197], off
	s_nop 0
	global_load_dwordx4 v[204:207], v[198:199], off
	global_load_dword v250, v[248:249], off offset:128
	global_load_dword v251, v[238:239], off offset:128
	s_waitcnt lgkmcnt(1)
	v_mfma_f32_16x16x32_bf16 v[166:169], v[126:129], v[190:193], v[166:169]
	ds_read2_b64 v[126:129], v160 offset0:96 offset1:100
	v_sub_f32_e32 v9, v131, v136
	v_mul_f32_e32 v9, 0x3fb8aa3b, v9
	s_waitcnt lgkmcnt(0)
	v_mfma_f32_16x16x32_bf16 v[174:177], v[126:129], v[190:193], v[174:177]
	v_exp_f32_e32 v127, v9
	v_sub_f32_e32 v9, v139, v136
	v_mul_f32_e32 v9, 0x3fb8aa3b, v9
	v_exp_f32_e32 v126, v9
	v_sub_f32_e32 v9, v130, v136
	v_mul_f32_e32 v9, 0x3fb8aa3b, v9
	v_exp_f32_e32 v129, v9
	v_sub_f32_e32 v9, v137, v136
	v_mul_f32_e32 v9, 0x3fb8aa3b, v9
	v_exp_f32_e32 v128, v9
	v_sub_f32_e32 v9, v135, v136
	v_mul_f32_e32 v9, 0x3fb8aa3b, v9
	v_exp_f32_e32 v131, v9
	v_sub_f32_e32 v9, v142, v136
	v_mul_f32_e32 v9, 0x3fb8aa3b, v9
	v_mfma_f32_16x16x32_bf16 v[170:173], v[186:189], v[190:193], v[170:173]
	s_waitcnt vmcnt(7)
	ds_write_b128 v75, v[182:185] offset:18432
	s_waitcnt vmcnt(6)
	ds_write_b128 v75, v[200:203] offset:27648
	s_waitcnt lgkmcnt(0)
	s_barrier
	v_exp_f32_e32 v130, v9
	v_sub_f32_e32 v9, v134, v136
	ds_read2_b64 v[182:185], v162 offset1:4
	ds_read2_b64 v[186:189], v161 offset0:32 offset1:36
	v_mul_f32_e32 v9, 0x3fb8aa3b, v9
	v_exp_f32_e32 v133, v9
	v_sub_f32_e32 v9, v138, v136
	v_mul_f32_e32 v9, 0x3fb8aa3b, v9
	v_exp_f32_e32 v134, v9
	v_lshl_add_u64 v[198:199], s[24:25], 1, v[78:79]
	v_lshl_add_u64 v[200:201], v[198:199], 0, v[70:71]
	v_cvt_pk_bf16_f32 v190, v127, v129
	v_cvt_pk_bf16_f32 v191, v131, v133
	v_cvt_pk_bf16_f32 v192, v126, v128
	v_cvt_pk_bf16_f32 v193, v130, v134
	v_lshl_add_u64 v[138:139], v[198:199], 0, v[80:81]
	v_sub_f32_e32 v9, v141, v136
	s_waitcnt lgkmcnt(1)
	v_mfma_f32_16x16x32_bf16 v[178:181], v[182:185], v[190:193], v[178:181]
	global_load_dwordx4 v[182:185], v[200:201], off
	s_nop 0
	global_load_dwordx4 v[198:201], v[138:139], off
	v_mul_f32_e32 v9, 0x3fb8aa3b, v9
	v_exp_f32_e32 v137, v9
	s_waitcnt lgkmcnt(0)
	v_mfma_f32_16x16x32_bf16 v[166:169], v[186:189], v[190:193], v[166:169]
	ds_read2_b64 v[186:189], v163 offset0:64 offset1:68
	v_sub_f32_e32 v9, v149, v136
	v_mul_f32_e32 v9, 0x3fb8aa3b, v9
	s_waitcnt lgkmcnt(0)
	v_mfma_f32_16x16x32_bf16 v[170:173], v[186:189], v[190:193], v[170:173]
	ds_read2_b64 v[186:189], v164 offset0:96 offset1:100
	v_exp_f32_e32 v135, v9
	v_sub_f32_e32 v9, v140, v136
	v_mul_f32_e32 v9, 0x3fb8aa3b, v9
	v_exp_f32_e32 v139, v9
	v_sub_f32_e32 v9, v145, v136
	v_mul_f32_e32 v9, 0x3fb8aa3b, v9
	v_exp_f32_e32 v138, v9
	v_sub_f32_e32 v9, v144, v136
	v_mul_f32_e32 v9, 0x3fb8aa3b, v9
	s_waitcnt lgkmcnt(0)
	v_mfma_f32_16x16x32_bf16 v[174:177], v[186:189], v[190:193], v[174:177]
	s_waitcnt vmcnt(5)
	ds_write_b128 v75, v[194:197]
	s_waitcnt vmcnt(4)
	ds_write_b128 v75, v[204:207] offset:9216
	s_waitcnt lgkmcnt(0)
	s_barrier
	v_exp_f32_e32 v141, v9
	v_sub_f32_e32 v9, v152, v136
	ds_read2_b64 v[186:189], v8 offset1:4
	v_mul_f32_e32 v9, 0x3fb8aa3b, v9
	ds_read2_b64 v[194:197], v7 offset0:32 offset1:36
	v_exp_f32_e32 v140, v9
	v_sub_f32_e32 v9, v143, v136
	v_sub_f32_e32 v8, v148, v136
	v_mul_f32_e32 v9, 0x3fb8aa3b, v9
	v_mul_f32_e32 v8, 0x3fb8aa3b, v8
	v_exp_f32_e32 v142, v9
	v_exp_f32_e32 v143, v8
	v_cvt_pk_bf16_f32 v190, v137, v139
	v_cvt_pk_bf16_f32 v192, v135, v138
	v_cvt_pk_bf16_f32 v191, v141, v142
	v_cvt_pk_bf16_f32 v193, v140, v143
	v_lshl_add_u64 v[8:9], s[26:27], 1, v[78:79]
	v_sub_f32_e32 v145, v153, v136
	s_waitcnt lgkmcnt(1)
	v_mfma_f32_16x16x32_bf16 v[178:181], v[186:189], v[190:193], v[178:181]
	ds_read2_b64 v[186:189], v6 offset0:64 offset1:68
	v_lshl_add_u64 v[6:7], v[8:9], 0, v[70:71]
	v_lshl_add_u64 v[8:9], v[8:9], 0, v[80:81]
	s_waitcnt lgkmcnt(1)
	v_mfma_f32_16x16x32_bf16 v[166:169], v[194:197], v[190:193], v[166:169]
	v_lshl_add_u64 v[248:249], v[6:7], 0, 0
	v_lshl_add_u64 v[238:239], v[8:9], 0, 0
	global_load_dwordx4 v[194:197], v[6:7], off
	global_load_dwordx4 v[202:205], v[8:9], off
	global_load_dword v250, v[248:249], off offset:128
	global_load_dword v251, v[238:239], off offset:128
	ds_read2_b64 v[78:81], v160 offset0:96 offset1:100
	s_waitcnt vmcnt(5)
	ds_write_b128 v75, v[182:185] offset:18432
	s_waitcnt vmcnt(4)
	ds_write_b128 v75, v[198:201] offset:27648
	s_waitcnt lgkmcnt(2)
	v_mfma_f32_16x16x32_bf16 v[174:177], v[78:81], v[190:193], v[174:177]
	s_waitcnt lgkmcnt(0)
	s_barrier
; #define LAS __attribute__((address_space(3)))
; __device__ __forceinline__ unsigned cvt_pk_bf16(float lo, float hi) { const float __attribute__((ext_vector_type(2))) v = {lo, hi}; return __builtin_bit_cast(unsigned, __builtin_convertvector(v, bf16x2_t)); }
; template <bool LOCAL>
; __device__ __forceinline__ void na_unit(const bf16* P, const bf16* VT, bf16* YCAT, const LAS float* rpb_l, LAS bf16* buf, int b, int gr, int hp, int qblk, int tid) {
;     ...
;             const int c = sidx - NCH;
;             if (LOCAL && c < 8) {
;                 float p[8];
; #pragma unroll
;                 for (int e = 0; e < 4; ++e) { p[e] = __expf(sl[2 * (c < 8 ? c : 0)][e] - m); p[4 + e] = __expf(sl[2 * (c < 8 ? c : 0) + 1][e] - m); }
; #pragma unroll
;                 for (int e = 0; e < 8; ++e) lsum += p[e];
;                 const bf16x8 pf = __builtin_bit_cast(bf16x8, (v4u){pg8::cvt_pk_bf16(p[0], p[1]), pg8::cvt_pk_bf16(p[2], p[3]), pg8::cvt_pk_bf16(p[4], p[5]), pg8::cvt_pk_bf16(p[6], p[7])});
; #pragma unroll
;                 for (int dt = 0; dt < 4; ++dt) { const LAS bf16* vp = cb + (16 * dt + fr) * 72 + kc0 + 4 * fq;
;                     o[dt] = __builtin_amdgcn_mfma_f32_16x16x32_bf16(frag44(vp, vp + 16), pf, o[dt], 0, 0, 0); }
;             } else {
;                 const int cc = c - NLOC;
; #pragma unroll
;                 for (int p2 = 0; p2 < 2; ++p2) {
;                     float p[8];
; #pragma unroll
;                     for (int e = 0; e < 4; ++e) { p[e] = __expf(sc[4 * (cc >= 0 ? cc : 0) + 2 * p2][e] - m); p[4 + e] = __expf(sc[4 * (cc >= 0 ? cc : 0) + 2 * p2 + 1][e] - m); }
; #pragma unroll
;                     for (int e = 0; e < 8; ++e) lsum += p[e];
;                     const bf16x8 pf = __builtin_bit_cast(bf16x8, (v4u){pg8::cvt_pk_bf16(p[0], p[1]), pg8::cvt_pk_bf16(p[2], p[3]), pg8::cvt_pk_bf16(p[4], p[5]), pg8::cvt_pk_bf16(p[6], p[7])});
; #pragma unroll
;                     for (int dt = 0; dt < 4; ++dt) { const LAS bf16* vp = cb + (16 * dt + fr) * 72 + 32 * p2 + 4 * fq;
;                         o[dt] = __builtin_amdgcn_mfma_f32_16x16x32_bf16(frag44(vp, vp + 16), pf, o[dt], 0, 0, 0); }
	v_sub_f32_e32 v70, v151, v136
	v_sub_f32_e32 v79, v150, v136
	v_sub_f32_e32 v81, v154, v136
	ds_read2_b64 v[150:153], v162 offset1:4
	v_mul_f32_e32 v70, 0x3fb8aa3b, v70
	v_mul_f32_e32 v79, 0x3fb8aa3b, v79
	v_mul_f32_e32 v81, 0x3fb8aa3b, v81
	v_mul_f32_e32 v145, 0x3fb8aa3b, v145
	v_exp_f32_e32 v78, v70
	v_sub_f32_e32 v70, v157, v136
	v_exp_f32_e32 v80, v79
	v_sub_f32_e32 v79, v155, v136
	v_exp_f32_e32 v144, v81
	v_sub_f32_e32 v81, v159, v136
	v_exp_f32_e32 v148, v145
	v_sub_f32_e32 v145, v156, v136
	v_mul_f32_e32 v70, 0x3fb8aa3b, v70
	v_mul_f32_e32 v79, 0x3fb8aa3b, v79
	v_mul_f32_e32 v81, 0x3fb8aa3b, v81
	v_mul_f32_e32 v145, 0x3fb8aa3b, v145
	v_exp_f32_e32 v70, v70
	v_exp_f32_e32 v79, v79
	v_exp_f32_e32 v81, v81
	v_exp_f32_e32 v145, v145
	v_cvt_pk_bf16_f32 v154, v78, v80
	v_cvt_pk_bf16_f32 v155, v144, v148
	v_cvt_pk_bf16_f32 v156, v70, v79
	v_cvt_pk_bf16_f32 v157, v81, v145
	v_mfma_f32_16x16x32_bf16 v[170:173], v[186:189], v[190:193], v[170:173]
	v_mul_f32_e32 v64, 0x3fb8aa3b, v64
	v_mul_f32_e32 v65, 0x3fb8aa3b, v65
	v_exp_f32_e32 v149, v62
	s_waitcnt lgkmcnt(0)
	v_mfma_f32_16x16x32_bf16 v[150:153], v[150:153], v[154:157], v[178:181]
	v_fma_f32 v62, v66, s72, -v136
	v_exp_f32_e32 v66, v63
	v_fma_f32 v63, v67, s72, -v136
	ds_read2_b64 v[178:181], v161 offset0:32 offset1:36
	ds_read2_b64 v[160:163], v163 offset0:64 offset1:68
	s_waitcnt lgkmcnt(0)
	v_mfma_f32_16x16x32_bf16 v[160:163], v[160:163], v[154:157], v[170:173]
	s_nop 2
	ds_read2_b64 v[170:173], v164 offset0:96 offset1:100
	v_exp_f32_e32 v67, v64
	v_fma_f32 v64, v68, s72, -v136
	v_mfma_f32_16x16x32_bf16 v[166:169], v[178:181], v[154:157], v[166:169]
	v_lshl_add_u64 v[248:249], v[6:7], 0, 0
	v_lshl_add_u64 v[238:239], v[8:9], 0, 0
	global_load_dwordx4 v[178:181], v[6:7], off offset:128
	global_load_dwordx4 v[182:185], v[8:9], off offset:128
	global_load_dword v250, v[248:249], off offset:256
	global_load_dword v251, v[238:239], off offset:256
	s_waitcnt vmcnt(7)
	ds_write_b128 v75, v[194:197]
	s_waitcnt vmcnt(6)
	ds_write_b128 v75, v[202:205] offset:9216
	s_waitcnt lgkmcnt(0)
	v_mfma_f32_16x16x32_bf16 v[154:157], v[170:173], v[154:157], v[174:177]
	s_barrier
	ds_read2_b64 v[170:173], v158 offset1:4
	v_exp_f32_e32 v68, v65
	v_fma_f32 v65, v69, s72, -v136
	v_mul_f32_e32 v62, 0x3fb8aa3b, v62
	v_mul_f32_e32 v63, 0x3fb8aa3b, v63
	v_mul_f32_e32 v64, 0x3fb8aa3b, v64
	v_mul_f32_e32 v65, 0x3fb8aa3b, v65
	v_exp_f32_e32 v62, v62
	v_exp_f32_e32 v63, v63
	v_exp_f32_e32 v64, v64
	v_exp_f32_e32 v65, v65
	v_cvt_pk_bf16_f32 v174, v149, v66
	v_cvt_pk_bf16_f32 v175, v67, v68
	v_cvt_pk_bf16_f32 v176, v62, v63
	v_cvt_pk_bf16_f32 v177, v64, v65
	v_add_u32_e32 v159, 0x800, v158
	v_add_u32_e32 v194, 0x1000, v158
	s_waitcnt lgkmcnt(0)
	v_mfma_f32_16x16x32_bf16 v[150:153], v[170:173], v[174:177], v[150:153]
	ds_read2_b64 v[170:173], v159 offset0:32 offset1:36
	v_add_u32_e32 v195, 0x1800, v158
	v_fma_f32 v58, v58, s72, -v136
	s_waitcnt lgkmcnt(0)
	v_mfma_f32_16x16x32_bf16 v[164:167], v[170:173], v[174:177], v[166:169]
	s_nop 2
	ds_read2_b64 v[168:171], v194 offset0:64 offset1:68
	v_fma_f32 v54, v54, s72, -v136
	v_fma_f32 v59, v59, s72, -v136
	s_waitcnt lgkmcnt(0)
	v_mfma_f32_16x16x32_bf16 v[160:163], v[168:171], v[174:177], v[160:163]
	ds_read2_b64 v[168:171], v195 offset0:96 offset1:100
	v_fma_f32 v55, v55, s72, -v136
	v_fma_f32 v60, v60, s72, -v136
	s_waitcnt lgkmcnt(0)
	v_mfma_f32_16x16x32_bf16 v[154:157], v[168:171], v[174:177], v[154:157]
	ds_read2_b64 v[168:171], v158 offset0:8 offset1:12
	v_fma_f32 v56, v56, s72, -v136
	v_fma_f32 v61, v61, s72, -v136
	v_fma_f32 v57, v57, s72, -v136
	v_mul_f32_e32 v58, 0x3fb8aa3b, v58
	v_mul_f32_e32 v54, 0x3fb8aa3b, v54
	v_mul_f32_e32 v59, 0x3fb8aa3b, v59
	v_mul_f32_e32 v55, 0x3fb8aa3b, v55
	v_mul_f32_e32 v60, 0x3fb8aa3b, v60
	v_mul_f32_e32 v56, 0x3fb8aa3b, v56
	v_mul_f32_e32 v61, 0x3fb8aa3b, v61
	v_mul_f32_e32 v57, 0x3fb8aa3b, v57
	v_exp_f32_e32 v58, v58
	v_exp_f32_e32 v54, v54
	v_exp_f32_e32 v59, v59
	v_exp_f32_e32 v55, v55
	v_exp_f32_e32 v60, v60
	v_exp_f32_e32 v56, v56
	v_exp_f32_e32 v61, v61
	v_exp_f32_e32 v57, v57
	v_cvt_pk_bf16_f32 v172, v58, v59
	v_cvt_pk_bf16_f32 v174, v54, v55
	v_cvt_pk_bf16_f32 v173, v60, v61
	v_cvt_pk_bf16_f32 v175, v56, v57
	v_fma_f32 v46, v46, s72, -v136
	v_fma_f32 v47, v47, s72, -v136
	s_waitcnt lgkmcnt(0)
	v_mfma_f32_16x16x32_bf16 v[150:153], v[168:171], v[172:175], v[150:153]
	ds_read2_b64 v[168:171], v159 offset0:40 offset1:44
	v_fma_f32 v48, v48, s72, -v136
	v_mul_f32_e32 v46, 0x3fb8aa3b, v46
	s_waitcnt lgkmcnt(0)
	v_mfma_f32_16x16x32_bf16 v[164:167], v[168:171], v[172:175], v[164:167]
	ds_read2_b64 v[168:171], v194 offset0:72 offset1:76
	v_mul_f32_e32 v47, 0x3fb8aa3b, v47
	v_mul_f32_e32 v48, 0x3fb8aa3b, v48
	s_waitcnt lgkmcnt(0)
	v_mfma_f32_16x16x32_bf16 v[160:163], v[168:171], v[172:175], v[160:163]
	ds_read2_b64 v[168:171], v195 offset0:104 offset1:108
	v_exp_f32_e32 v69, v46
	v_fma_f32 v46, v50, s72, -v136
	v_exp_f32_e32 v50, v47
	v_fma_f32 v47, v51, s72, -v136
	v_exp_f32_e32 v51, v48
	v_fma_f32 v48, v52, s72, -v136
	v_add_u32_e32 v52, 0x4800, v158
	v_lshl_add_u64 v[248:249], v[6:7], 0, 0
	v_lshl_add_u64 v[238:239], v[8:9], 0, 0
	global_load_dwordx4 v[186:189], v[6:7], off offset:256
	global_load_dwordx4 v[190:193], v[8:9], off offset:256
	global_load_dword v250, v[248:249], off offset:384
	global_load_dword v251, v[238:239], off offset:384
	s_waitcnt lgkmcnt(0)
	v_mfma_f32_16x16x32_bf16 v[154:157], v[168:171], v[172:175], v[154:157]
	s_waitcnt vmcnt(7)
	ds_write_b128 v75, v[178:181] offset:18432
	s_waitcnt vmcnt(6)
	ds_write_b128 v75, v[182:185] offset:27648
	s_waitcnt lgkmcnt(0)
	s_barrier
; #define LAS __attribute__((address_space(3)))
; __device__ __forceinline__ unsigned cvt_pk_bf16(float lo, float hi) { const float __attribute__((ext_vector_type(2))) v = {lo, hi}; return __builtin_bit_cast(unsigned, __builtin_convertvector(v, bf16x2_t)); }
; #define NA_STORE(sidx) do { LAS bf16* d_ = buf + ((sidx) & 1) * 9216; _Pragma("unroll") for (int q_ = 0; q_ < 2; ++q_) *(LAS v4u*)(d_ + q_ * 4608 + lrow * 72 + lseg * 8) = ld[(sidx) & 1][q_]; } while (0)
; template <bool LOCAL>
; __device__ __forceinline__ void na_unit(const bf16* P, const bf16* VT, bf16* YCAT, const LAS float* rpb_l, LAS bf16* buf, int b, int gr, int hp, int qblk, int tid) {
;     ...
;             } else {
;                 const int cc = c - NLOC;
; #pragma unroll
;                 for (int p2 = 0; p2 < 2; ++p2) {
;                     float p[8];
; #pragma unroll
;                     for (int e = 0; e < 4; ++e) { p[e] = __expf(sc[4 * (cc >= 0 ? cc : 0) + 2 * p2][e] - m); p[4 + e] = __expf(sc[4 * (cc >= 0 ? cc : 0) + 2 * p2 + 1][e] - m); }
; #pragma unroll
;                     for (int e = 0; e < 8; ++e) lsum += p[e];
;                     const bf16x8 pf = __builtin_bit_cast(bf16x8, (v4u){pg8::cvt_pk_bf16(p[0], p[1]), pg8::cvt_pk_bf16(p[2], p[3]), pg8::cvt_pk_bf16(p[4], p[5]), pg8::cvt_pk_bf16(p[6], p[7])});
; #pragma unroll
;                     for (int dt = 0; dt < 4; ++dt) { const LAS bf16* vp = cb + (16 * dt + fr) * 72 + 32 * p2 + 4 * fq;
;                         o[dt] = __builtin_amdgcn_mfma_f32_16x16x32_bf16(frag44(vp, vp + 16), pf, o[dt], 0, 0, 0); }
;                 }
;             }
;         }
;         if (sidx + 1 < 2 * NCH) NA_STORE(sidx + 1);
;         __syncthreads();
	v_fma_f32 v49, v49, s72, -v136
	ds_read2_b64 v[168:171], v52 offset1:4
	v_mul_f32_e32 v49, 0x3fb8aa3b, v49
	v_exp_f32_e32 v176, v49
	v_fma_f32 v49, v53, s72, -v136
	v_mul_f32_e32 v46, 0x3fb8aa3b, v46
	v_mul_f32_e32 v47, 0x3fb8aa3b, v47
	v_mul_f32_e32 v48, 0x3fb8aa3b, v48
	v_mul_f32_e32 v49, 0x3fb8aa3b, v49
	v_exp_f32_e32 v46, v46
	v_exp_f32_e32 v47, v47
	v_exp_f32_e32 v48, v48
	v_exp_f32_e32 v53, v49
	v_cvt_pk_bf16_f32 v172, v69, v50
	v_cvt_pk_bf16_f32 v173, v51, v176
	v_cvt_pk_bf16_f32 v174, v46, v47
	v_cvt_pk_bf16_f32 v175, v48, v53
	v_add_u32_e32 v177, 0x5000, v158
	v_add_u32_e32 v178, 0x5800, v158
	s_waitcnt lgkmcnt(0)
	v_mfma_f32_16x16x32_bf16 v[150:153], v[168:171], v[172:175], v[150:153]
	ds_read2_b64 v[168:171], v177 offset0:32 offset1:36
	v_add_u32_e32 v49, 0x6000, v158
	v_fma_f32 v38, v38, s72, -v136
	s_waitcnt lgkmcnt(0)
	v_mfma_f32_16x16x32_bf16 v[164:167], v[168:171], v[172:175], v[164:167]
	ds_read2_b64 v[168:171], v178 offset0:64 offset1:68
	v_mul_f32_e32 v38, 0x3fb8aa3b, v38
	v_fma_f32 v42, v42, s72, -v136
	s_waitcnt lgkmcnt(0)
	v_mfma_f32_16x16x32_bf16 v[160:163], v[168:171], v[172:175], v[160:163]
	ds_read2_b64 v[168:171], v49 offset0:96 offset1:100
	v_mul_f32_e32 v42, 0x3fb8aa3b, v42
	v_fma_f32 v30, v30, s72, -v136
	s_waitcnt lgkmcnt(0)
	v_mfma_f32_16x16x32_bf16 v[154:157], v[168:171], v[172:175], v[154:157]
	v_exp_f32_e32 v173, v38
	v_fma_f32 v38, v43, s72, -v136
	v_mul_f32_e32 v38, 0x3fb8aa3b, v38
	v_exp_f32_e32 v174, v38
	v_fma_f32 v38, v39, s72, -v136
	v_mul_f32_e32 v38, 0x3fb8aa3b, v38
	v_exp_f32_e32 v175, v38
	v_fma_f32 v38, v44, s72, -v136
	v_mul_f32_e32 v38, 0x3fb8aa3b, v38
	v_exp_f32_e32 v179, v38
	v_fma_f32 v38, v40, s72, -v136
	v_mul_f32_e32 v38, 0x3fb8aa3b, v38
	v_exp_f32_e32 v172, v42
	v_exp_f32_e32 v180, v38
	v_fma_f32 v38, v45, s72, -v136
	ds_read2_b64 v[42:45], v52 offset0:8 offset1:12
	v_mul_f32_e32 v38, 0x3fb8aa3b, v38
	v_exp_f32_e32 v181, v38
	v_fma_f32 v38, v41, s72, -v136
	v_mul_f32_e32 v38, 0x3fb8aa3b, v38
	v_exp_f32_e32 v182, v38
	v_cvt_pk_bf16_f32 v38, v172, v174
	v_cvt_pk_bf16_f32 v39, v179, v181
	v_cvt_pk_bf16_f32 v40, v173, v175
	v_cvt_pk_bf16_f32 v41, v180, v182
	v_mul_f32_e32 v30, 0x3fb8aa3b, v30
	v_fma_f32 v22, v22, s72, -v136
	s_waitcnt lgkmcnt(0)
	v_mfma_f32_16x16x32_bf16 v[42:45], v[42:45], v[38:41], v[150:153]
	v_mul_f32_e32 v22, 0x3fb8aa3b, v22
	v_fma_f32 v26, v26, s72, -v136
	v_mul_f32_e32 v26, 0x3fb8aa3b, v26
	ds_read2_b64 v[150:153], v177 offset0:40 offset1:44
	s_waitcnt lgkmcnt(0)
	v_mfma_f32_16x16x32_bf16 v[150:153], v[150:153], v[38:41], v[164:167]
	s_nop 2
	ds_read2_b64 v[164:167], v178 offset0:72 offset1:76
	v_fma_f32 v2, v2, s72, -v136
	v_mul_f32_e32 v2, 0x3fb8aa3b, v2
	s_waitcnt lgkmcnt(0)
	v_mfma_f32_16x16x32_bf16 v[160:163], v[164:167], v[38:41], v[160:163]
	ds_read2_b64 v[164:167], v49 offset0:104 offset1:108
	global_load_dwordx4 v[168:171], v[6:7], off offset:384
	s_nop 0
	global_load_dwordx4 v[6:9], v[8:9], off offset:384
	s_waitcnt vmcnt(5)
	ds_write_b128 v75, v[186:189]
	s_waitcnt vmcnt(4)
	ds_write_b128 v75, v[190:193] offset:9216
	s_waitcnt lgkmcnt(2)
	v_mfma_f32_16x16x32_bf16 v[38:41], v[164:167], v[38:41], v[154:157]
	v_exp_f32_e32 v164, v30
	v_fma_f32 v30, v34, s72, -v136
	v_mul_f32_e32 v30, 0x3fb8aa3b, v30
	v_exp_f32_e32 v165, v30
	v_fma_f32 v30, v31, s72, -v136
	v_mul_f32_e32 v30, 0x3fb8aa3b, v30
	v_exp_f32_e32 v166, v30
	v_fma_f32 v30, v35, s72, -v136
	v_mul_f32_e32 v30, 0x3fb8aa3b, v30
	v_exp_f32_e32 v167, v30
	v_fma_f32 v30, v32, s72, -v136
	v_mul_f32_e32 v30, 0x3fb8aa3b, v30
	v_exp_f32_e32 v183, v30
	v_fma_f32 v30, v36, s72, -v136
	v_mul_f32_e32 v30, 0x3fb8aa3b, v30
	v_exp_f32_e32 v184, v30
	v_fma_f32 v30, v33, s72, -v136
	s_waitcnt lgkmcnt(0)
	s_barrier
	v_mul_f32_e32 v34, 0x3fb8aa3b, v30
	ds_read2_b64 v[30:33], v158 offset1:4
	v_exp_f32_e32 v185, v34
	v_fma_f32 v34, v37, s72, -v136
	v_mul_f32_e32 v34, 0x3fb8aa3b, v34
	v_exp_f32_e32 v186, v34
	v_cvt_pk_bf16_f32 v34, v164, v166
	v_cvt_pk_bf16_f32 v35, v183, v185
	v_cvt_pk_bf16_f32 v36, v165, v167
	v_cvt_pk_bf16_f32 v37, v184, v186
	ds_read2_b64 v[154:157], v195 offset0:96 offset1:100
	v_fma_f32 v10, v10, s72, -v136
	s_waitcnt lgkmcnt(1)
	v_mfma_f32_16x16x32_bf16 v[30:33], v[30:33], v[34:37], v[42:45]
	v_mul_f32_e32 v10, 0x3fb8aa3b, v10
	s_nop 1
	ds_read2_b64 v[42:45], v159 offset0:32 offset1:36
	s_waitcnt lgkmcnt(0)
	v_mfma_f32_16x16x32_bf16 v[42:45], v[42:45], v[34:37], v[150:153]
	s_nop 2
	ds_read2_b64 v[150:153], v194 offset0:64 offset1:68
	s_waitcnt lgkmcnt(0)
	v_mfma_f32_16x16x32_bf16 v[150:153], v[150:153], v[34:37], v[160:163]
	v_mfma_f32_16x16x32_bf16 v[34:37], v[154:157], v[34:37], v[38:41]
	v_exp_f32_e32 v155, v22
	v_fma_f32 v22, v27, s72, -v136
	v_mul_f32_e32 v22, 0x3fb8aa3b, v22
	v_exp_f32_e32 v156, v22
	v_fma_f32 v22, v23, s72, -v136
	v_mul_f32_e32 v22, 0x3fb8aa3b, v22
	v_exp_f32_e32 v157, v22
	v_fma_f32 v22, v28, s72, -v136
	v_mul_f32_e32 v22, 0x3fb8aa3b, v22
	v_exp_f32_e32 v160, v22
	v_fma_f32 v22, v24, s72, -v136
	v_mul_f32_e32 v22, 0x3fb8aa3b, v22
	v_exp_f32_e32 v154, v26
	v_exp_f32_e32 v161, v22
	v_fma_f32 v22, v29, s72, -v136
	ds_read2_b64 v[26:29], v158 offset0:8 offset1:12
	v_mul_f32_e32 v22, 0x3fb8aa3b, v22
	v_exp_f32_e32 v158, v22
	v_fma_f32 v22, v25, s72, -v136
	v_mul_f32_e32 v22, 0x3fb8aa3b, v22
	v_exp_f32_e32 v162, v22
	v_cvt_pk_bf16_f32 v22, v154, v156
	v_cvt_pk_bf16_f32 v23, v160, v158
	v_cvt_pk_bf16_f32 v24, v155, v157
	v_cvt_pk_bf16_f32 v25, v161, v162
	ds_read2_b64 v[38:41], v194 offset0:72 offset1:76
	s_waitcnt lgkmcnt(1)
	v_mfma_f32_16x16x32_bf16 v[26:29], v[26:29], v[22:25], v[30:33]
	s_nop 2
	ds_read2_b64 v[30:33], v159 offset0:40 offset1:44
	s_waitcnt lgkmcnt(0)
	v_mfma_f32_16x16x32_bf16 v[30:33], v[30:33], v[22:25], v[42:45]
	s_nop 2
	ds_read2_b64 v[42:45], v195 offset0:104 offset1:108
	s_waitcnt vmcnt(1)
	ds_write_b128 v75, v[168:171] offset:18432
	s_waitcnt vmcnt(0)
	ds_write_b128 v75, v[6:9] offset:27648
	v_fma_f32 v6, v14, s72, -v136
	v_mul_f32_e32 v6, 0x3fb8aa3b, v6
	v_mfma_f32_16x16x32_bf16 v[38:41], v[38:41], v[22:25], v[150:153]
	s_waitcnt lgkmcnt(0)
	s_barrier
; #define LAS __attribute__((address_space(3)))
; __device__ __forceinline__ unsigned cvt_pk_bf16(float lo, float hi) { const float __attribute__((ext_vector_type(2))) v = {lo, hi}; return __builtin_bit_cast(unsigned, __builtin_convertvector(v, bf16x2_t)); }
; #define NA_STORE(sidx) do { LAS bf16* d_ = buf + ((sidx) & 1) * 9216; _Pragma("unroll") for (int q_ = 0; q_ < 2; ++q_) *(LAS v4u*)(d_ + q_ * 4608 + lrow * 72 + lseg * 8) = ld[(sidx) & 1][q_]; } while (0)
; template <bool LOCAL>
; __device__ __forceinline__ void na_unit(const bf16* P, const bf16* VT, bf16* YCAT, const LAS float* rpb_l, LAS bf16* buf, int b, int gr, int hp, int qblk, int tid) {
;     ...
;             } else {
;                 const int cc = c - NLOC;
; #pragma unroll
;                 for (int p2 = 0; p2 < 2; ++p2) {
;                     float p[8];
; #pragma unroll
;                     for (int e = 0; e < 4; ++e) { p[e] = __expf(sc[4 * (cc >= 0 ? cc : 0) + 2 * p2][e] - m); p[4 + e] = __expf(sc[4 * (cc >= 0 ? cc : 0) + 2 * p2 + 1][e] - m); }
; #pragma unroll
;                     for (int e = 0; e < 8; ++e) lsum += p[e];
;                     const bf16x8 pf = __builtin_bit_cast(bf16x8, (v4u){pg8::cvt_pk_bf16(p[0], p[1]), pg8::cvt_pk_bf16(p[2], p[3]), pg8::cvt_pk_bf16(p[4], p[5]), pg8::cvt_pk_bf16(p[6], p[7])});
; #pragma unroll
;                     for (int dt = 0; dt < 4; ++dt) { const LAS bf16* vp = cb + (16 * dt + fr) * 72 + 32 * p2 + 4 * fq;
;                         o[dt] = __builtin_amdgcn_mfma_f32_16x16x32_bf16(frag44(vp, vp + 16), pf, o[dt], 0, 0, 0); }
;                 }
;             }
;         }
;         if (sidx + 1 < 2 * NCH) NA_STORE(sidx + 1);
;         __syncthreads();
;     }
;     ...
;     lsum += __shfl_xor(lsum, 16); lsum += __shfl_xor(lsum, 32);
;     const float inv = 1.f / lsum;
	v_mfma_f32_16x16x32_bf16 v[22:25], v[42:45], v[22:25], v[34:37]
	v_ashrrev_i32_e32 v75, 31, v74
	s_nop 1
	v_exp_f32_e32 v34, v6
	v_fma_f32 v6, v18, s72, -v136
	v_mul_f32_e32 v6, 0x3fb8aa3b, v6
	v_exp_f32_e32 v35, v6
	v_fma_f32 v6, v15, s72, -v136
	v_mul_f32_e32 v6, 0x3fb8aa3b, v6
	v_exp_f32_e32 v36, v6
	v_fma_f32 v6, v19, s72, -v136
	v_mul_f32_e32 v6, 0x3fb8aa3b, v6
	v_exp_f32_e32 v37, v6
	v_fma_f32 v6, v16, s72, -v136
	v_mul_f32_e32 v6, 0x3fb8aa3b, v6
	v_exp_f32_e32 v42, v6
	v_fma_f32 v6, v20, s72, -v136
	v_mul_f32_e32 v6, 0x3fb8aa3b, v6
	v_exp_f32_e32 v43, v6
	v_fma_f32 v6, v17, s72, -v136
	v_mul_f32_e32 v14, 0x3fb8aa3b, v6
	ds_read2_b64 v[6:9], v52 offset1:4
	v_exp_f32_e32 v44, v14
	v_fma_f32 v14, v21, s72, -v136
	v_mul_f32_e32 v14, 0x3fb8aa3b, v14
	v_exp_f32_e32 v45, v14
	v_cvt_pk_bf16_f32 v14, v34, v36
	v_cvt_pk_bf16_f32 v15, v42, v44
	v_cvt_pk_bf16_f32 v16, v35, v37
	v_cvt_pk_bf16_f32 v17, v43, v45
	ds_read2_b64 v[18:21], v177 offset0:32 offset1:36
	s_waitcnt lgkmcnt(1)
	v_mfma_f32_16x16x32_bf16 v[6:9], v[6:9], v[14:17], v[26:29]
	s_nop 2
	ds_read2_b64 v[26:29], v178 offset0:64 offset1:68
	s_waitcnt lgkmcnt(0)
	v_mfma_f32_16x16x32_bf16 v[26:29], v[26:29], v[14:17], v[38:41]
	s_nop 2
	v_add_f32_e32 v38, 0, v132
	v_add_f32_e32 v38, v96, v38
	v_add_f32_e32 v38, v95, v38
	v_add_f32_e32 v38, v99, v38
	v_add_f32_e32 v38, v92, v38
	v_add_f32_e32 v38, v91, v38
	v_add_f32_e32 v38, v94, v38
	v_add_f32_e32 v38, v93, v38
	v_add_f32_e32 v38, v86, v38
	v_add_f32_e32 v38, v90, v38
	v_add_f32_e32 v38, v98, v38
	v_add_f32_e32 v38, v100, v38
	v_add_f32_e32 v38, v76, v38
	v_add_f32_e32 v38, v87, v38
	v_add_f32_e32 v38, v97, v38
	v_add_f32_e32 v38, v101, v38
	v_add_f32_e32 v38, v103, v38
	v_add_f32_e32 v38, v105, v38
	v_add_f32_e32 v38, v107, v38
	v_add_f32_e32 v38, v108, v38
	v_add_f32_e32 v38, v102, v38
	v_add_f32_e32 v38, v104, v38
	v_add_f32_e32 v38, v106, v38
	v_add_f32_e32 v38, v109, v38
	v_add_f32_e32 v38, v111, v38
	v_add_f32_e32 v38, v113, v38
	v_add_f32_e32 v38, v115, v38
	v_add_f32_e32 v38, v116, v38
	v_add_f32_e32 v38, v110, v38
	v_add_f32_e32 v38, v112, v38
	v_add_f32_e32 v38, v114, v38
	v_add_f32_e32 v38, v117, v38
	v_add_f32_e32 v38, v119, v38
	v_add_f32_e32 v38, v121, v38
	v_add_f32_e32 v38, v123, v38
	v_add_f32_e32 v38, v124, v38
	v_add_f32_e32 v38, v118, v38
	v_add_f32_e32 v38, v120, v38
	v_add_f32_e32 v38, v122, v38
	v_add_f32_e32 v38, v125, v38
	v_add_f32_e32 v38, v127, v38
	v_add_f32_e32 v38, v129, v38
	v_add_f32_e32 v38, v131, v38
	v_add_f32_e32 v38, v133, v38
	v_add_f32_e32 v38, v126, v38
	v_add_f32_e32 v38, v128, v38
	v_add_f32_e32 v38, v130, v38
	v_add_f32_e32 v38, v134, v38
	v_add_f32_e32 v38, v137, v38
	v_add_f32_e32 v38, v139, v38
	v_add_f32_e32 v38, v141, v38
	v_add_f32_e32 v38, v142, v38
	v_add_f32_e32 v38, v135, v38
	v_add_f32_e32 v38, v138, v38
	v_add_f32_e32 v38, v140, v38
	v_add_f32_e32 v38, v143, v38
	v_add_f32_e32 v38, v78, v38
	v_add_f32_e32 v38, v80, v38
	v_add_f32_e32 v38, v144, v38
	v_add_f32_e32 v38, v148, v38
	v_add_f32_e32 v38, v70, v38
	v_add_f32_e32 v38, v79, v38
	v_add_f32_e32 v38, v81, v38
	v_add_f32_e32 v38, v145, v38
	v_add_f32_e32 v38, v149, v38
	v_add_f32_e32 v38, v66, v38
	v_add_f32_e32 v38, v67, v38
	v_add_f32_e32 v38, v68, v38
	v_add_f32_e32 v38, v62, v38
	v_add_f32_e32 v38, v63, v38
	v_add_f32_e32 v38, v64, v38
	v_add_f32_e32 v38, v65, v38
	v_add_f32_e32 v38, v58, v38
	v_add_f32_e32 v38, v59, v38
	v_add_f32_e32 v38, v60, v38
	v_add_f32_e32 v38, v61, v38
	v_add_f32_e32 v38, v54, v38
	v_add_f32_e32 v38, v55, v38
	v_add_f32_e32 v38, v56, v38
	v_add_f32_e32 v38, v57, v38
	v_add_f32_e32 v38, v69, v38
	v_add_f32_e32 v38, v50, v38
	v_add_f32_e32 v38, v51, v38
	v_add_f32_e32 v38, v176, v38
	v_add_f32_e32 v38, v46, v38
	v_add_f32_e32 v38, v47, v38
	v_add_f32_e32 v38, v48, v38
	v_add_f32_e32 v38, v53, v38
	v_add_f32_e32 v38, v172, v38
	v_mfma_f32_16x16x32_bf16 v[18:21], v[18:21], v[14:17], v[30:33]
	v_add_f32_e32 v38, v174, v38
	v_add_f32_e32 v38, v179, v38
	v_add_f32_e32 v38, v181, v38
	ds_read2_b64 v[30:33], v49 offset0:96 offset1:100
	v_add_f32_e32 v38, v173, v38
	v_add_f32_e32 v38, v175, v38
	v_add_f32_e32 v38, v180, v38
	v_add_f32_e32 v38, v182, v38
	v_add_f32_e32 v38, v164, v38
	v_add_f32_e32 v38, v166, v38
	s_waitcnt lgkmcnt(0)
	v_mfma_f32_16x16x32_bf16 v[14:17], v[30:33], v[14:17], v[22:25]
	v_add_f32_e32 v38, v183, v38
	s_nop 1
	v_exp_f32_e32 v23, v2
	v_fma_f32 v2, v11, s72, -v136
	v_mul_f32_e32 v2, 0x3fb8aa3b, v2
	v_add_f32_e32 v38, v185, v38
	v_exp_f32_e32 v24, v2
	v_fma_f32 v2, v3, s72, -v136
	v_add_f32_e32 v38, v165, v38
	v_mul_f32_e32 v2, 0x3fb8aa3b, v2
	v_add_f32_e32 v38, v167, v38
	v_exp_f32_e32 v25, v2
	v_fma_f32 v2, v12, s72, -v136
	v_add_f32_e32 v38, v184, v38
	v_mul_f32_e32 v2, 0x3fb8aa3b, v2
	v_add_f32_e32 v38, v186, v38
	v_exp_f32_e32 v30, v2
	v_fma_f32 v2, v4, s72, -v136
	v_add_f32_e32 v38, v154, v38
	v_mul_f32_e32 v2, 0x3fb8aa3b, v2
	v_add_f32_e32 v38, v156, v38
	v_exp_f32_e32 v22, v10
	v_exp_f32_e32 v31, v2
	v_fma_f32 v2, v13, s72, -v136
	ds_read2_b64 v[10:13], v52 offset0:8 offset1:12
	v_add_f32_e32 v38, v160, v38
	v_mul_f32_e32 v2, 0x3fb8aa3b, v2
	v_add_f32_e32 v38, v158, v38
	v_exp_f32_e32 v32, v2
	v_fma_f32 v2, v5, s72, -v136
	v_add_f32_e32 v38, v155, v38
	v_mul_f32_e32 v2, 0x3fb8aa3b, v2
	v_add_f32_e32 v38, v157, v38
	v_exp_f32_e32 v33, v2
	v_add_f32_e32 v38, v161, v38
	v_add_f32_e32 v38, v162, v38
	v_add_f32_e32 v34, v34, v38
	v_add_f32_e32 v34, v36, v34
	v_cvt_pk_bf16_f32 v2, v22, v24
	v_cvt_pk_bf16_f32 v3, v30, v32
	v_cvt_pk_bf16_f32 v4, v23, v25
	v_cvt_pk_bf16_f32 v5, v31, v33
	v_add_f32_e32 v34, v42, v34
	v_add_f32_e32 v34, v44, v34
	s_waitcnt lgkmcnt(0)
	v_mfma_f32_16x16x32_bf16 v[6:9], v[10:13], v[2:5], v[6:9]
	ds_read2_b64 v[10:13], v177 offset0:40 offset1:44
	v_add_f32_e32 v34, v35, v34
	v_add_f32_e32 v34, v37, v34
	v_add_f32_e32 v34, v43, v34
	v_add_f32_e32 v34, v45, v34
	v_add_f32_e32 v22, v22, v34
	v_add_f32_e32 v22, v24, v22
	v_add_f32_e32 v22, v30, v22
	v_add_f32_e32 v22, v32, v22
	s_waitcnt lgkmcnt(0)
	v_mfma_f32_16x16x32_bf16 v[10:13], v[10:13], v[2:5], v[18:21]
	v_add_f32_e32 v22, v23, v22
	v_add_f32_e32 v22, v25, v22
	v_add_f32_e32 v22, v31, v22
	ds_read2_b64 v[18:21], v178 offset0:72 offset1:76
	v_add_f32_e32 v30, v33, v22
	ds_bpermute_b32 v31, v88, v30
	ds_read2_b64 v[22:25], v49 offset0:104 offset1:108
	s_waitcnt lgkmcnt(2)
	v_mfma_f32_16x16x32_bf16 v[18:21], v[18:21], v[2:5], v[26:29]
	s_waitcnt lgkmcnt(1)
	s_nop 1
	v_add_f32_e32 v26, v30, v31
	ds_bpermute_b32 v27, v89, v26
	v_lshlrev_b32_e32 v70, 1, v77
	s_waitcnt lgkmcnt(1)
	v_mfma_f32_16x16x32_bf16 v[14:17], v[22:25], v[2:5], v[14:17]
	s_waitcnt lgkmcnt(0)
	s_barrier
; __device__ __forceinline__ unsigned cvt_pk_bf16(float lo, float hi) { const float __attribute__((ext_vector_type(2))) v = {lo, hi}; return __builtin_bit_cast(unsigned, __builtin_convertvector(v, bf16x2_t)); }
; template <bool LOCAL>
; __device__ __forceinline__ void na_unit(const bf16* P, const bf16* VT, bf16* YCAT, const LAS float* rpb_l, LAS bf16* buf, int b, int gr, int hp, int qblk, int tid) {
;     ...
;     lsum += __shfl_xor(lsum, 16); lsum += __shfl_xor(lsum, 32);
;     const float inv = 1.f / lsum;
;     bf16* op = YCAT + (size_t)(qrow0 + fr) * D + 512 + h * 64 + 4 * fq;
; #pragma unroll
;     for (int dt = 0; dt < 4; ++dt) { v2u w; w.x = pg8::cvt_pk_bf16(o[dt][0] * inv, o[dt][1] * inv); w.y = pg8::cvt_pk_bf16(o[dt][2] * inv, o[dt][3] * inv); *(v2u*)(op + dt * 16) = w; }
	v_add_f32_e32 v2, v26, v27
	v_div_scale_f32 v3, s[0:1], v2, v2, 1.0
	v_rcp_f32_e32 v4, v3
	s_nop 0
	v_fma_f32 v5, -v3, v4, 1.0
	v_fmac_f32_e32 v4, v5, v4
	v_div_scale_f32 v5, vcc, 1.0, v2, 1.0
	v_mul_f32_e32 v22, v5, v4
	v_fma_f32 v23, -v3, v22, v5
	v_fmac_f32_e32 v22, v23, v4
	v_fma_f32 v3, -v3, v22, v5
	v_div_fmas_f32 v3, v3, v4, v22
	v_div_fixup_f32 v22, v3, v2, 1.0
	v_lshlrev_b64 v[2:3], 11, v[74:75]
	v_lshl_add_u64 v[2:3], s[10:11], 0, v[2:3]
	v_lshl_add_u64 v[2:3], v[72:73], 1, v[2:3]
	v_pk_mul_f32 v[6:7], v[6:7], v[22:23] op_sel_hi:[1,0]
	v_pk_mul_f32 v[8:9], v[8:9], v[22:23] op_sel_hi:[1,0]
	v_lshl_add_u64 v[4:5], v[2:3], 0, v[70:71]
	v_cvt_pk_bf16_f32 v6, v6, v7
	v_cvt_pk_bf16_f32 v7, v8, v9
	global_store_dwordx2 v[4:5], v[6:7], off offset:1024
	v_pk_mul_f32 v[6:7], v[10:11], v[22:23] op_sel_hi:[1,0]
	v_pk_mul_f32 v[8:9], v[12:13], v[22:23] op_sel_hi:[1,0]
	v_cvt_pk_bf16_f32 v6, v6, v7
	v_cvt_pk_bf16_f32 v7, v8, v9
	global_store_dwordx2 v[4:5], v[6:7], off offset:1056
	v_pk_mul_f32 v[6:7], v[18:19], v[22:23] op_sel_hi:[1,0]
	v_pk_mul_f32 v[8:9], v[20:21], v[22:23] op_sel_hi:[1,0]
	v_cvt_pk_bf16_f32 v6, v6, v7
	v_cvt_pk_bf16_f32 v7, v8, v9
	v_lshl_add_u64 v[2:3], v[4:5], 0, s[12:13]
	global_store_dwordx2 v[4:5], v[6:7], off offset:1088
	v_pk_mul_f32 v[4:5], v[14:15], v[22:23] op_sel_hi:[1,0]
	v_pk_mul_f32 v[6:7], v[16:17], v[22:23] op_sel_hi:[1,0]
	v_cvt_pk_bf16_f32 v4, v4, v5

; #define LAS __attribute__((address_space(3)))
; template <bool LOCAL>
; __device__ __forceinline__ void na_unit(const bf16* P, const bf16* VT, bf16* YCAT, const LAS float* rpb_l, LAS bf16* buf, int b, int gr, int hp, int qblk, int tid) {
;     typedef pg8::bf16x8 bf16x8;
;     constexpr int NCH = LOCAL ? 12 : 4, NLOC = LOCAL ? 8 : 0;
;     const int lane = tid & 63, wv = tid >> 6, fr = lane & 15, fq = lane >> 4, hh = wv >> 2, qb = wv & 3, h = 2 * hp + hh;
;     const int qrow0 = LOCAL ? NCTX + b * SEQ + gr * 64 + 16 * qb : b * CTXL + qblk * 64 + 16 * qb;
;     const int r0 = min(max(gr - 4, 0), 24);
;     const int kc0 = qb == 0 ? 0 : qb == 1 ? 8 : qb == 2 ? 24 : 32;
;     const int qcol = 16 * qb + fr, cs = min(max(qcol - 8, 0), 48);
;     const LAS float* rpb = rpb_l + h * 15 * 31;
;     v4u ld[2][2];
;     const int lrow = (tid >> 3) & 63, lseg = tid & 7;
;     ...
;     bf16x8 qf[2];
; #pragma unroll
;     for (int ks = 0; ks < 2; ++ks) qf[ks] = *(const bf16x8*)(P + (size_t)(qrow0 + fr) * DINP + h * 64 + 32 * ks + 8 * fq);
;     f32x4 sl[16], sc[16];
;     float m = -1.0e30f, lsum = 0.f;
;     f32x4 o[4];
; #pragma unroll
;     for (int dt = 0; dt < 4; ++dt) o[dt] = (f32x4){0.f, 0.f, 0.f, 0.f};
;     NA_ISSUE(0); NA_ISSUE(1); NA_STORE(0);
;     __syncthreads();
; #pragma unroll
;     for (int sidx = 0; sidx < 2 * NCH; ++sidx) {
;         if (sidx + 2 < 2 * NCH) NA_ISSUE(sidx + 2);
;         const LAS bf16* cb = buf + (sidx & 1) * 9216 + hh * 4608;
;         if (sidx < NCH) {
;             const int c = sidx;
;             if (LOCAL && c < 8) {
; #pragma unroll
;                 for (int t2 = 0; t2 < 2; ++t2) {
;                     const LAS bf16* kp = cb + (kc0 + 16 * t2 + fr) * 72 + 8 * fq;
;                     f32x4 acc = {0.f, 0.f, 0.f, 0.f};
;                     acc = __builtin_amdgcn_mfma_f32_16x16x32_bf16(*(const LAS bf16x8*)(kp), qf[0], acc, 0, 0, 0);
;                     acc = __builtin_amdgcn_mfma_f32_16x16x32_bf16(*(const LAS bf16x8*)(kp + 32), qf[1], acc, 0, 0, 0);
;                     const LAS float* rb = rpb + (r0 + c - gr + 7) * 31 + 15 - qcol;
; #pragma unroll
;                     for (int e = 0; e < 4; ++e) { const int kcol = kc0 + 16 * t2 + 4 * fq + e; const bool ok = (kcol >= cs) && (kcol < cs + 16);
;                         const float sv = ok ? acc[e] * 0.125f + rb[ok ? kcol : qcol] : -1.0e30f; acc[e] = sv; m = fmaxf(m, sv); }
.LBB0_1498:
	v_mov_b32_e32 v93, v0
	s_movk_i32 s2, 0x2400
	v_and_b32_e32 v89, 15, v93
	v_bfe_u32 v91, v93, 4, 2
	v_ashrrev_i32_e32 v92, 8, v93
	s_mov_b64 s[0:1], -1
	s_cmpk_gt_i32 s76, 0x7ff
	v_bfe_u32 v88, v93, 3, 6
	v_lshlrev_b32_e32 v76, 3, v91
	v_lshlrev_b32_e32 v70, 4, v91
	v_mad_i32_i24 v86, v92, s2, 0
	v_mul_u32_u24_e32 v87, 0x90, v89
	s_waitcnt lgkmcnt(0)
	s_barrier
	s_cbranch_scc0 .LBB0_1500
	s_lshl_b32 s0, s76, 4
	s_and_b32 s0, s0, 0xffffff00
	s_addk_i32 s0, 0x8000
	v_mov_b64_e32 v[78:79], s[8:9]
	s_lshl_b32 s1, s76, 5
	v_or_b32_e32 v77, s0, v88
	v_lshlrev_b32_e32 v4, 4, v93
	s_and_b32 s16, s1, 0x180
	v_mad_u64_u32 v[2:3], s[14:15], v77, s69, v[78:79]
	v_and_b32_e32 v80, 0x70, v4
	v_mov_b32_e32 v81, v71
	v_lshl_add_u64 v[2:3], v[2:3], 0, v[80:81]
	s_lshl_b32 s2, s16, 1
	v_lshl_add_u64 v[2:3], v[2:3], 0, s[2:3]
	global_load_dwordx4 v[6:9], v[2:3], off offset:1024
	global_load_dwordx4 v[10:13], v[2:3], off offset:1152
	s_lshl_b32 s1, s76, 6
	s_and_b32 s1, s1, 0xc0
	v_lshrrev_b32_e32 v2, 2, v93
	v_and_or_b32 v2, v2, 48, s1
	v_lshl_add_u32 v4, v92, 6, s16
	v_or3_b32 v72, v2, v89, s0
	v_ashrrev_i32_e32 v5, 31, v4
	v_mad_u64_u32 v[2:3], s[14:15], v72, s69, v[78:79]
	v_lshlrev_b64 v[74:75], 1, v[4:5]
	v_lshl_add_u64 v[2:3], v[2:3], 0, v[74:75]
	v_or_b32_e32 v14, 64, v77
	v_lshl_add_u64 v[22:23], v[2:3], 0, v[70:71]
	v_mad_u64_u32 v[14:15], s[14:15], v14, s69, v[78:79]
	global_load_dwordx4 v[2:5], v[22:23], off
	v_lshl_add_u64 v[14:15], v[14:15], 0, v[80:81]
	v_lshl_add_u64 v[18:19], v[14:15], 0, s[2:3]
	s_mov_b32 s100, 0x60000
	s_mov_b32 s101, 0
	v_lshl_add_u64 v[248:249], v[18:19], 0, s[100:101]
	global_load_dwordx4 v[14:17], v[18:19], off offset:1024
	s_nop 0
	global_load_dwordx4 v[18:21], v[18:19], off offset:1152
	global_load_dword v250, v[248:249], off offset:1024
	global_load_dword v251, v[248:249], off offset:1152
	s_nop 0
	global_load_dwordx4 v[50:53], v[22:23], off offset:64
	v_mul_u32_u24_e32 v22, 0x90, v88
	v_add3_u32 v73, 0, v22, v80
	v_or_b32_e32 v22, 0x80, v77
	v_add3_u32 v90, v86, v70, v87
	s_mov_b32 s1, s3
	v_cmp_lt_i32_e32 vcc, v83, v84
	s_waitcnt vmcnt(7)
	ds_write_b128 v73, v[6:9]
	s_waitcnt vmcnt(6)
	ds_write_b128 v73, v[10:13] offset:9216
	v_mad_u64_u32 v[10:11], s[14:15], v22, s69, v[78:79]
	v_lshl_add_u64 v[10:11], v[10:11], 0, v[80:81]
	v_lshl_add_u64 v[26:27], v[10:11], 0, s[2:3]
	s_waitcnt lgkmcnt(0)
	s_barrier
	ds_read_b128 v[6:9], v90
	ds_read_b128 v[10:13], v90 offset:2304
	v_lshl_add_u64 v[248:249], v[26:27], 0, s[100:101]
	global_load_dwordx4 v[22:25], v[26:27], off offset:1024
	global_load_dwordx4 v[30:33], v[26:27], off offset:1152
	global_load_dword v250, v[248:249], off offset:1024
	global_load_dword v251, v[248:249], off offset:1152
	ds_read_b128 v[26:29], v90 offset:64
	ds_read_b128 v[34:37], v90 offset:4608
	ds_read_b128 v[38:41], v90 offset:2368
	ds_read_b128 v[42:45], v90 offset:4672
	ds_read_b128 v[46:49], v90 offset:6912
	s_waitcnt vmcnt(9) lgkmcnt(6)
	v_mfma_f32_16x16x32_bf16 v[6:9], v[6:9], v[2:5], 0
	ds_read_b128 v[54:57], v90 offset:6976
	s_waitcnt vmcnt(8)
	ds_write_b128 v73, v[14:17] offset:18432
	s_waitcnt vmcnt(7)
	ds_write_b128 v73, v[18:21] offset:27648
	s_waitcnt lgkmcnt(0)
	v_mfma_f32_16x16x32_bf16 v[10:13], v[10:13], v[2:5], 0
	s_barrier
	v_mfma_f32_16x16x32_bf16 v[14:17], v[34:37], v[2:5], 0
	v_mfma_f32_16x16x32_bf16 v[18:21], v[46:49], v[2:5], 0
	ds_read_b128 v[34:37], v90 offset:18432
	ds_read_b128 v[46:49], v90 offset:18496
	ds_read_b128 v[58:61], v90 offset:20736
	ds_read_b128 v[94:97], v90 offset:20800
	s_waitcnt vmcnt(4)
	v_mfma_f32_16x16x32_bf16 v[62:65], v[26:29], v[50:53], v[6:9]
	s_nop 2
	v_or_b32_e32 v6, s16, v88
	s_waitcnt lgkmcnt(1)
	v_mfma_f32_16x16x32_bf16 v[98:101], v[58:61], v[2:5], 0
	ds_read_b128 v[58:61], v90 offset:23040
	ds_read_b128 v[102:105], v90 offset:23104
	v_mul_u32_u24_e32 v8, 0x9000, v6
	v_mov_b32_e32 v7, v71
	v_mfma_f32_16x16x32_bf16 v[66:69], v[38:41], v[50:53], v[10:13]
	v_mov_b32_e32 v9, v71
	s_nop 1
	v_lshl_add_u64 v[10:11], s[4:5], 0, v[80:81]
	v_or_b32_e32 v12, 64, v6
	v_or_b32_e32 v13, 0xc0, v77
	v_lshl_add_u64 v[10:11], s[0:1], 1, v[10:11]
	v_lshlrev_b32_e32 v6, 1, v8
	v_mul_u32_u24_e32 v8, 0x9000, v12
	v_mad_u64_u32 v[12:13], s[0:1], v13, s69, v[78:79]
	v_lshl_add_u64 v[78:79], v[10:11], 0, v[6:7]
	v_lshlrev_b32_e32 v8, 1, v8
	v_lshl_add_u64 v[6:7], v[12:13], 0, v[80:81]
	v_lshl_add_u64 v[80:81], v[10:11], 0, v[8:9]
	v_lshl_add_u64 v[10:11], v[6:7], 0, s[2:3]
	s_waitcnt lgkmcnt(1)
	v_mfma_f32_16x16x32_bf16 v[106:109], v[58:61], v[2:5], 0
	ds_read_b128 v[58:61], v90 offset:25344
	ds_read_b128 v[110:113], v90 offset:25408
	global_load_dwordx4 v[6:9], v[10:11], off offset:1024
	s_nop 0
	global_load_dwordx4 v[10:13], v[10:11], off offset:1152
	v_mul_f32_e32 v38, 0x3e000000, v68
	s_waitcnt lgkmcnt(1)
	v_mfma_f32_16x16x32_bf16 v[114:117], v[58:61], v[2:5], 0
	v_mul_f32_e32 v39, 0x3e000000, v69
	s_waitcnt vmcnt(5)
	ds_write_b128 v73, v[22:25]
	s_waitcnt vmcnt(4)
	ds_write_b128 v73, v[30:33] offset:9216
	v_mfma_f32_16x16x32_bf16 v[58:61], v[42:45], v[50:53], v[14:17]
	s_waitcnt lgkmcnt(0)
	s_barrier
; #define LAS __attribute__((address_space(3)))
; template <bool LOCAL>
; __device__ __forceinline__ void na_unit(const bf16* P, const bf16* VT, bf16* YCAT, const LAS float* rpb_l, LAS bf16* buf, int b, int gr, int hp, int qblk, int tid) {
;     ...
;                 const int cc = c - NLOC;
; #pragma unroll
;                 for (int t4 = 0; t4 < 4; ++t4) {
;                     const LAS bf16* kp = cb + (16 * t4 + fr) * 72 + 8 * fq;
;                     f32x4 acc = {0.f, 0.f, 0.f, 0.f};
;                     acc = __builtin_amdgcn_mfma_f32_16x16x32_bf16(*(const LAS bf16x8*)(kp), qf[0], acc, 0, 0, 0);
;                     acc = __builtin_amdgcn_mfma_f32_16x16x32_bf16(*(const LAS bf16x8*)(kp + 32), qf[1], acc, 0, 0, 0);
; #pragma unroll
;                     for (int e = 0; e < 4; ++e) { acc[e] *= 0.125f; m = fmaxf(m, acc[e]); }
;                     sc[4 * (cc >= 0 ? cc : 0) + t4] = acc; }
;             }
;             if (sidx == NCH - 1) { m = fmaxf(m, __shfl_xor(m, 16)); m = fmaxf(m, __shfl_xor(m, 32)); }
	s_nop 0
	v_mul_f32_e32 v14, 0x3e000000, v62
	v_mul_f32_e32 v15, 0x3e000000, v63
	v_mfma_f32_16x16x32_bf16 v[54:57], v[54:57], v[50:53], v[18:21]
	s_nop 1
	v_mul_f32_e32 v40, 0x3e000000, v58
	v_mul_f32_e32 v41, 0x3e000000, v59
	v_mul_f32_e32 v77, 0x3e000000, v60
	v_mfma_f32_16x16x32_bf16 v[42:45], v[94:97], v[50:53], v[98:101]
	v_mul_f32_e32 v18, 0x3e000000, v64
	v_mul_f32_e32 v19, 0x3e000000, v65
	v_mul_f32_e32 v20, 0x3e000000, v66
	v_max3_f32 v99, v14, s74, v15
	v_mul_f32_e32 v21, 0x3e000000, v67
	v_max3_f32 v18, v99, v18, v19
	v_mfma_f32_16x16x32_bf16 v[34:37], v[34:37], v[2:5], 0
	v_max3_f32 v18, v18, v20, v21
	ds_read_b128 v[14:17], v90
	v_max3_f32 v22, v18, v38, v39
	ds_read_b128 v[18:21], v90 offset:2304
	v_mul_f32_e32 v94, 0x3e000000, v61
	v_max3_f32 v22, v22, v40, v41
	v_mul_f32_e32 v95, 0x3e000000, v54
	v_mul_f32_e32 v96, 0x3e000000, v55
	v_max3_f32 v38, v22, v77, v94
	v_mfma_f32_16x16x32_bf16 v[46:49], v[46:49], v[50:53], v[34:37]
	v_mul_f32_e32 v97, 0x3e000000, v56
	v_mul_f32_e32 v98, 0x3e000000, v57
	v_max3_f32 v38, v38, v95, v96
	ds_read_b128 v[22:25], v90 offset:64
	ds_read_b128 v[30:33], v90 offset:4608
	v_max3_f32 v38, v38, v97, v98
	ds_read_b128 v[94:97], v90 offset:2368
	v_mfma_f32_16x16x32_bf16 v[34:37], v[102:105], v[50:53], v[106:109]
	v_mul_f32_e32 v100, 0x3e000000, v46
	v_mul_f32_e32 v101, 0x3e000000, v47
	v_mul_f32_e32 v102, 0x3e000000, v48
	v_mul_f32_e32 v103, 0x3e000000, v49
	v_max3_f32 v38, v38, v100, v101
	v_mul_f32_e32 v106, 0x3e000000, v42
	v_mul_f32_e32 v107, 0x3e000000, v43
	s_waitcnt lgkmcnt(4)
	v_mfma_f32_16x16x32_bf16 v[14:17], v[14:17], v[2:5], 0
	v_max3_f32 v38, v38, v102, v103
	v_mul_f32_e32 v108, 0x3e000000, v44
	v_mul_f32_e32 v109, 0x3e000000, v45
	s_waitcnt lgkmcnt(3)
	v_mfma_f32_16x16x32_bf16 v[18:21], v[18:21], v[2:5], 0
	ds_read_b128 v[98:101], v90 offset:4672
	s_waitcnt lgkmcnt(2)
	v_mfma_f32_16x16x32_bf16 v[102:105], v[30:33], v[2:5], 0
	v_max3_f32 v30, v38, v106, v107
	v_max3_f32 v30, v30, v108, v109
	v_mfma_f32_16x16x32_bf16 v[26:29], v[110:113], v[50:53], v[114:117]
	v_mul_f32_e32 v110, 0x3e000000, v34
	v_mul_f32_e32 v111, 0x3e000000, v35
	v_mul_f32_e32 v112, 0x3e000000, v36
	v_mul_f32_e32 v113, 0x3e000000, v37
	v_max3_f32 v30, v30, v110, v111
	v_mfma_f32_16x16x32_bf16 v[38:41], v[22:25], v[50:53], v[14:17]
	s_nop 1
	v_mul_f32_e32 v114, 0x3e000000, v26
	v_mul_f32_e32 v115, 0x3e000000, v27
	v_mul_f32_e32 v116, 0x3e000000, v28
	v_max3_f32 v14, v30, v112, v113
	s_waitcnt lgkmcnt(1)
	v_mfma_f32_16x16x32_bf16 v[30:33], v[94:97], v[50:53], v[18:21]
	v_lshl_add_u64 v[248:249], v[78:79], 0, 0
	v_lshl_add_u64 v[238:239], v[80:81], 0, 0
	global_load_dwordx4 v[94:97], v[78:79], off
	global_load_dwordx4 v[106:109], v[80:81], off
	global_load_dword v250, v[248:249], off offset:128
	global_load_dword v251, v[238:239], off offset:128
	v_mul_f32_e32 v117, 0x3e000000, v29
	v_max3_f32 v14, v14, v114, v115
	v_max3_f32 v22, v14, v116, v117
	ds_read_b128 v[14:17], v90 offset:6912
	v_mul_f32_e32 v23, 0x3e000000, v38
	v_mul_f32_e32 v24, 0x3e000000, v39
	v_mul_f32_e32 v25, 0x3e000000, v40
	v_mul_f32_e32 v77, 0x3e000000, v41
	v_max3_f32 v22, v22, v23, v24
	s_waitcnt lgkmcnt(1)
	v_mfma_f32_16x16x32_bf16 v[18:21], v[98:101], v[50:53], v[102:105]
	v_mul_f32_e32 v98, 0x3e000000, v30
	v_mul_f32_e32 v99, 0x3e000000, v31
	v_max3_f32 v22, v22, v25, v77
	v_max3_f32 v77, v22, v98, v99
	ds_read_b128 v[22:25], v90 offset:6976
	s_waitcnt vmcnt(5)
	ds_write_b128 v73, v[6:9] offset:18432
	s_waitcnt vmcnt(4)
	ds_write_b128 v73, v[10:13] offset:27648
	s_waitcnt lgkmcnt(0)
	s_barrier
	ds_read_b128 v[6:9], v90 offset:18432
	v_mul_f32_e32 v100, 0x3e000000, v32
	v_mul_f32_e32 v10, 0x3e000000, v33
	v_mfma_f32_16x16x32_bf16 v[14:17], v[14:17], v[2:5], 0
	v_max3_f32 v77, v77, v100, v10
	ds_read_b128 v[10:13], v90 offset:18496
	v_mul_f32_e32 v98, 0x3e000000, v18
	v_mfma_f32_16x16x32_bf16 v[22:25], v[22:25], v[50:53], v[14:17]
	v_mul_f32_e32 v99, 0x3e000000, v21
	ds_read_b128 v[110:113], v90 offset:25408
	s_nop 1
	v_mul_f32_e32 v14, 0x3e000000, v19
	v_max3_f32 v77, v77, v98, v14
	s_waitcnt lgkmcnt(2)
	v_mfma_f32_16x16x32_bf16 v[6:9], v[6:9], v[2:5], 0
	ds_read_b128 v[14:17], v90 offset:20736
	v_mul_f32_e32 v98, 0x3e000000, v20
	v_max3_f32 v77, v77, v98, v99
	s_waitcnt lgkmcnt(2)
	v_mfma_f32_16x16x32_bf16 v[10:13], v[10:13], v[50:53], v[6:9]
	v_mul_f32_e32 v98, 0x3e000000, v22
	v_mul_f32_e32 v99, 0x3e000000, v23
	v_max3_f32 v77, v77, v98, v99
	ds_read_b128 v[6:9], v90 offset:20800
	s_waitcnt lgkmcnt(1)
	v_mfma_f32_16x16x32_bf16 v[14:17], v[14:17], v[2:5], 0
	ds_read_b128 v[98:101], v90 offset:23040
	v_mul_f32_e32 v102, 0x3e000000, v24
	v_mul_f32_e32 v103, 0x3e000000, v25
	s_waitcnt lgkmcnt(1)
	v_mfma_f32_16x16x32_bf16 v[14:17], v[6:9], v[50:53], v[14:17]
	ds_read_b128 v[6:9], v90 offset:23104
	v_max3_f32 v77, v77, v102, v103
	ds_read_b128 v[102:105], v90 offset:25344
	s_waitcnt lgkmcnt(2)
	v_mfma_f32_16x16x32_bf16 v[98:101], v[98:101], v[2:5], 0
	v_mul_f32_e32 v114, 0x3e000000, v10
	v_mul_f32_e32 v115, 0x3e000000, v11
	v_mul_f32_e32 v116, 0x3e000000, v12
	s_waitcnt lgkmcnt(1)
	v_mfma_f32_16x16x32_bf16 v[6:9], v[6:9], v[50:53], v[98:101]
	v_mul_f32_e32 v117, 0x3e000000, v13
	v_max3_f32 v77, v77, v114, v115
	v_mul_f32_e32 v118, 0x3e000000, v14
	v_mul_f32_e32 v119, 0x3e000000, v15
	s_waitcnt lgkmcnt(0)
	v_mfma_f32_16x16x32_bf16 v[2:5], v[102:105], v[2:5], 0
	v_max3_f32 v77, v77, v116, v117
	v_mul_f32_e32 v90, 0x3e000000, v16
	v_mul_f32_e32 v98, 0x3e000000, v17
	v_max3_f32 v77, v77, v118, v119
	v_mul_f32_e32 v99, 0x3e000000, v6
	v_mul_f32_e32 v100, 0x3e000000, v7
	v_max3_f32 v77, v77, v90, v98
	v_mul_f32_e32 v101, 0x3e000000, v8
	v_mul_f32_e32 v102, 0x3e000000, v9
	v_max3_f32 v77, v77, v99, v100
	v_mfma_f32_16x16x32_bf16 v[2:5], v[110:113], v[50:53], v[2:5]
	v_max3_f32 v77, v77, v101, v102
	v_lshl_add_u64 v[248:249], v[78:79], 0, 0
	v_lshl_add_u64 v[238:239], v[80:81], 0, 0
	global_load_dwordx4 v[98:101], v[78:79], off offset:128
	global_load_dwordx4 v[102:105], v[80:81], off offset:128
	global_load_dword v250, v[248:249], off offset:256
	global_load_dword v251, v[238:239], off offset:256
	s_waitcnt vmcnt(7)
	ds_write_b128 v73, v[94:97]
	s_waitcnt vmcnt(6)
	ds_write_b128 v73, v[106:109] offset:9216
	s_nop 0
	v_mul_f32_e32 v50, 0x3e000000, v2
	v_mul_f32_e32 v51, 0x3e000000, v3
	v_mul_f32_e32 v52, 0x3e000000, v4
	v_mul_f32_e32 v53, 0x3e000000, v5
	v_max3_f32 v50, v77, v50, v51
	v_max3_f32 v51, v50, v52, v53
	v_cndmask_b32_e32 v50, v82, v83, vcc
	v_lshlrev_b32_e32 v50, 2, v50
	ds_bpermute_b32 v52, v50, v51
	v_cmp_lt_i32_e32 vcc, v85, v84
	s_waitcnt lgkmcnt(0)
	s_barrier
; #define LAS __attribute__((address_space(3)))
; __device__ __forceinline__ unsigned cvt_pk_bf16(float lo, float hi) { const float __attribute__((ext_vector_type(2))) v = {lo, hi}; return __builtin_bit_cast(unsigned, __builtin_convertvector(v, bf16x2_t)); }
; template <bool LOCAL>
; __device__ __forceinline__ void na_unit(const bf16* P, const bf16* VT, bf16* YCAT, const LAS float* rpb_l, LAS bf16* buf, int b, int gr, int hp, int qblk, int tid) {
;     ...
;             if (sidx == NCH - 1) { m = fmaxf(m, __shfl_xor(m, 16)); m = fmaxf(m, __shfl_xor(m, 32)); }
;         } else {
;             const int c = sidx - NCH;
;             if (LOCAL && c < 8) {
;                 float p[8];
; #pragma unroll
;                 for (int e = 0; e < 4; ++e) { p[e] = __expf(sl[2 * (c < 8 ? c : 0)][e] - m); p[4 + e] = __expf(sl[2 * (c < 8 ? c : 0) + 1][e] - m); }
; #pragma unroll
;                 for (int e = 0; e < 8; ++e) lsum += p[e];
;                 const bf16x8 pf = __builtin_bit_cast(bf16x8, (v4u){pg8::cvt_pk_bf16(p[0], p[1]), pg8::cvt_pk_bf16(p[2], p[3]), pg8::cvt_pk_bf16(p[4], p[5]), pg8::cvt_pk_bf16(p[6], p[7])});
; #pragma unroll
;                 for (int dt = 0; dt < 4; ++dt) { const LAS bf16* vp = cb + (16 * dt + fr) * 72 + kc0 + 4 * fq;
;                     o[dt] = __builtin_amdgcn_mfma_f32_16x16x32_bf16(frag44(vp, vp + 16), pf, o[dt], 0, 0, 0); }
;             } else {
;                 const int cc = c - NLOC;
; #pragma unroll
;                 for (int p2 = 0; p2 < 2; ++p2) {
;                     float p[8];
; #pragma unroll
;                     for (int e = 0; e < 4; ++e) { p[e] = __expf(sc[4 * (cc >= 0 ? cc : 0) + 2 * p2][e] - m); p[4 + e] = __expf(sc[4 * (cc >= 0 ? cc : 0) + 2 * p2 + 1][e] - m); }
; #pragma unroll
;                     for (int e = 0; e < 8; ++e) lsum += p[e];
;                     const bf16x8 pf = __builtin_bit_cast(bf16x8, (v4u){pg8::cvt_pk_bf16(p[0], p[1]), pg8::cvt_pk_bf16(p[2], p[3]), pg8::cvt_pk_bf16(p[4], p[5]), pg8::cvt_pk_bf16(p[6], p[7])});
; #pragma unroll
;                     for (int dt = 0; dt < 4; ++dt) { const LAS bf16* vp = cb + (16 * dt + fr) * 72 + 32 * p2 + 4 * fq;
;                         o[dt] = __builtin_amdgcn_mfma_f32_16x16x32_bf16(frag44(vp, vp + 16), pf, o[dt], 0, 0, 0); }
;                 }
;             }
;         }
;         if (sidx + 1 < 2 * NCH) NA_STORE(sidx + 1);
	v_max_f32_e32 v52, v52, v52
	v_max_f32_e32 v52, v51, v52
	v_cndmask_b32_e32 v51, v82, v85, vcc
	v_lshlrev_b32_e32 v51, 2, v51
	ds_bpermute_b32 v53, v51, v52
	s_waitcnt lgkmcnt(0)
	v_max_f32_e32 v53, v53, v53
	v_max_f32_e32 v77, v52, v53
	v_fma_f32 v52, v62, s71, -v77
	v_fma_f32 v64, v64, s71, -v77
	v_mul_f32_e32 v52, 0x3fb8aa3b, v52
	v_fma_f32 v62, v63, s71, -v77
	v_mul_f32_e32 v64, 0x3fb8aa3b, v64
	v_fma_f32 v65, v65, s71, -v77
	v_exp_f32_e32 v53, v52
	v_fma_f32 v52, v66, s71, -v77
	v_mul_f32_e32 v62, 0x3fb8aa3b, v62
	v_exp_f32_e32 v66, v64
	v_fma_f32 v64, v68, s71, -v77
	v_mul_f32_e32 v65, 0x3fb8aa3b, v65
	v_add3_u32 v68, v86, v76, v87
	v_exp_f32_e32 v63, v62
	v_fma_f32 v62, v67, s71, -v77
	v_exp_f32_e32 v67, v65
	v_fma_f32 v65, v69, s71, -v77
	v_add_u32_e32 v69, 0x800, v68
	v_add_u32_e32 v90, 0x1000, v68
	v_add_u32_e32 v134, 0x1800, v68
	ds_read2_b64 v[94:97], v68 offset1:4
	ds_read2_b64 v[110:113], v69 offset0:32 offset1:36
	ds_read2_b64 v[114:117], v90 offset0:64 offset1:68
	ds_read2_b64 v[118:121], v134 offset0:96 offset1:100
	v_mul_f32_e32 v52, 0x3fb8aa3b, v52
	v_mul_f32_e32 v62, 0x3fb8aa3b, v62
	v_mul_f32_e32 v64, 0x3fb8aa3b, v64
	v_mul_f32_e32 v65, 0x3fb8aa3b, v65
	v_exp_f32_e32 v52, v52
	v_exp_f32_e32 v62, v62
	v_exp_f32_e32 v64, v64
	v_exp_f32_e32 v65, v65
	v_cvt_pk_bf16_f32 v106, v53, v63
	v_cvt_pk_bf16_f32 v107, v66, v67
	v_cvt_pk_bf16_f32 v108, v52, v62
	v_cvt_pk_bf16_f32 v109, v64, v65
	v_fma_f32 v58, v58, s71, -v77
	v_fma_f32 v54, v54, s71, -v77
	s_waitcnt lgkmcnt(3)
	v_mfma_f32_16x16x32_bf16 v[94:97], v[94:97], v[106:109], 0
	v_fma_f32 v59, v59, s71, -v77
	v_fma_f32 v55, v55, s71, -v77
	v_fma_f32 v60, v60, s71, -v77
	s_waitcnt lgkmcnt(2)
	v_mfma_f32_16x16x32_bf16 v[110:113], v[110:113], v[106:109], 0
	v_fma_f32 v56, v56, s71, -v77
	v_fma_f32 v61, v61, s71, -v77
	v_fma_f32 v57, v57, s71, -v77
	s_waitcnt lgkmcnt(1)
	v_mfma_f32_16x16x32_bf16 v[114:117], v[114:117], v[106:109], 0
	v_mul_f32_e32 v58, 0x3fb8aa3b, v58
	v_mul_f32_e32 v54, 0x3fb8aa3b, v54
	v_mul_f32_e32 v59, 0x3fb8aa3b, v59
	s_waitcnt lgkmcnt(0)
	v_mfma_f32_16x16x32_bf16 v[106:109], v[118:121], v[106:109], 0
	ds_read2_b64 v[118:121], v68 offset0:8 offset1:12
	v_mul_f32_e32 v55, 0x3fb8aa3b, v55
	v_mul_f32_e32 v60, 0x3fb8aa3b, v60
	v_mul_f32_e32 v56, 0x3fb8aa3b, v56
	v_mul_f32_e32 v61, 0x3fb8aa3b, v61
	v_mul_f32_e32 v57, 0x3fb8aa3b, v57
	v_exp_f32_e32 v58, v58
	v_exp_f32_e32 v54, v54
	v_exp_f32_e32 v59, v59
	v_exp_f32_e32 v55, v55
	v_exp_f32_e32 v60, v60
	v_exp_f32_e32 v56, v56
	v_exp_f32_e32 v61, v61
	v_exp_f32_e32 v57, v57
	v_cvt_pk_bf16_f32 v122, v58, v59
	v_cvt_pk_bf16_f32 v124, v54, v55
	v_cvt_pk_bf16_f32 v123, v60, v61
	v_cvt_pk_bf16_f32 v125, v56, v57
	v_fma_f32 v42, v42, s71, -v77
	v_mul_f32_e32 v42, 0x3fb8aa3b, v42
	s_waitcnt lgkmcnt(0)
	v_mfma_f32_16x16x32_bf16 v[94:97], v[118:121], v[122:125], v[94:97]
	ds_read2_b64 v[118:121], v69 offset0:40 offset1:44
	v_fma_f32 v46, v46, s71, -v77
	v_mul_f32_e32 v46, 0x3fb8aa3b, v46
	s_waitcnt lgkmcnt(0)
	v_mfma_f32_16x16x32_bf16 v[110:113], v[118:121], v[122:125], v[110:113]
	ds_read2_b64 v[118:121], v90 offset0:72 offset1:76
	v_add_u32_e32 v136, 0x5000, v68
	v_fma_f32 v26, v26, s71, -v77
	s_waitcnt lgkmcnt(0)
	v_mfma_f32_16x16x32_bf16 v[114:117], v[118:121], v[122:125], v[114:117]
	ds_read2_b64 v[118:121], v134 offset0:104 offset1:108
	v_lshl_add_u64 v[248:249], v[78:79], 0, 0
	v_lshl_add_u64 v[238:239], v[80:81], 0, 0
	global_load_dwordx4 v[126:129], v[78:79], off offset:256
	global_load_dwordx4 v[130:133], v[80:81], off offset:256
	global_load_dword v250, v[248:249], off offset:384
	global_load_dword v251, v[238:239], off offset:384
	s_waitcnt vmcnt(7)
	ds_write_b128 v73, v[98:101] offset:18432
	s_waitcnt vmcnt(6)
	ds_write_b128 v73, v[102:105] offset:27648
	s_waitcnt lgkmcnt(2)
	v_mfma_f32_16x16x32_bf16 v[106:109], v[118:121], v[122:125], v[106:109]
	v_exp_f32_e32 v119, v42
	v_fma_f32 v42, v47, s71, -v77
	v_mul_f32_e32 v42, 0x3fb8aa3b, v42
	v_exp_f32_e32 v120, v42
	v_fma_f32 v42, v43, s71, -v77
	v_mul_f32_e32 v42, 0x3fb8aa3b, v42
	v_exp_f32_e32 v121, v42
	v_fma_f32 v42, v48, s71, -v77
	v_mul_f32_e32 v42, 0x3fb8aa3b, v42
	v_exp_f32_e32 v122, v42
	v_fma_f32 v42, v44, s71, -v77
	v_mul_f32_e32 v42, 0x3fb8aa3b, v42
	v_add_u32_e32 v124, 0x4800, v68
	s_waitcnt lgkmcnt(0)
	s_barrier
; #define LAS __attribute__((address_space(3)))
; __device__ __forceinline__ unsigned cvt_pk_bf16(float lo, float hi) { const float __attribute__((ext_vector_type(2))) v = {lo, hi}; return __builtin_bit_cast(unsigned, __builtin_convertvector(v, bf16x2_t)); }
; #define NA_STORE(sidx) do { LAS bf16* d_ = buf + ((sidx) & 1) * 9216; _Pragma("unroll") for (int q_ = 0; q_ < 2; ++q_) *(LAS v4u*)(d_ + q_ * 4608 + lrow * 72 + lseg * 8) = ld[(sidx) & 1][q_]; } while (0)
; template <bool LOCAL>
; __device__ __forceinline__ void na_unit(const bf16* P, const bf16* VT, bf16* YCAT, const LAS float* rpb_l, LAS bf16* buf, int b, int gr, int hp, int qblk, int tid) {
;     ...
;                 const int cc = c - NLOC;
; #pragma unroll
;                 for (int p2 = 0; p2 < 2; ++p2) {
;                     float p[8];
; #pragma unroll
;                     for (int e = 0; e < 4; ++e) { p[e] = __expf(sc[4 * (cc >= 0 ? cc : 0) + 2 * p2][e] - m); p[4 + e] = __expf(sc[4 * (cc >= 0 ? cc : 0) + 2 * p2 + 1][e] - m); }
; #pragma unroll
;                     for (int e = 0; e < 8; ++e) lsum += p[e];
;                     const bf16x8 pf = __builtin_bit_cast(bf16x8, (v4u){pg8::cvt_pk_bf16(p[0], p[1]), pg8::cvt_pk_bf16(p[2], p[3]), pg8::cvt_pk_bf16(p[4], p[5]), pg8::cvt_pk_bf16(p[6], p[7])});
; #pragma unroll
;                     for (int dt = 0; dt < 4; ++dt) { const LAS bf16* vp = cb + (16 * dt + fr) * 72 + 32 * p2 + 4 * fq;
;                         o[dt] = __builtin_amdgcn_mfma_f32_16x16x32_bf16(frag44(vp, vp + 16), pf, o[dt], 0, 0, 0); }
;                 }
;             }
;         }
;         if (sidx + 1 < 2 * NCH) NA_STORE(sidx + 1);
	v_exp_f32_e32 v118, v46
	v_exp_f32_e32 v123, v42
	v_fma_f32 v42, v49, s71, -v77
	ds_read2_b64 v[46:49], v124 offset1:4
	v_mul_f32_e32 v42, 0x3fb8aa3b, v42
	v_exp_f32_e32 v125, v42
	v_fma_f32 v42, v45, s71, -v77
	v_mul_f32_e32 v42, 0x3fb8aa3b, v42
	v_exp_f32_e32 v135, v42
	v_cvt_pk_bf16_f32 v42, v118, v120
	v_cvt_pk_bf16_f32 v43, v122, v125
	v_cvt_pk_bf16_f32 v44, v119, v121
	v_cvt_pk_bf16_f32 v45, v123, v135
	v_mul_f32_e32 v26, 0x3fb8aa3b, v26
	v_fma_f32 v34, v34, s71, -v77
	s_waitcnt lgkmcnt(0)
	v_mfma_f32_16x16x32_bf16 v[46:49], v[46:49], v[42:45], v[94:97]
	v_mul_f32_e32 v34, 0x3fb8aa3b, v34
	v_fma_f32 v30, v30, s71, -v77
	v_mul_f32_e32 v30, 0x3fb8aa3b, v30
	ds_read2_b64 v[94:97], v136 offset0:32 offset1:36
	s_waitcnt lgkmcnt(0)
	v_mfma_f32_16x16x32_bf16 v[94:97], v[94:97], v[42:45], v[110:113]
	s_nop 2
	v_add_u32_e32 v110, 0x5800, v68
	v_add_u32_e32 v111, 0x6000, v68
	ds_read2_b64 v[98:101], v110 offset0:64 offset1:68
	ds_read2_b64 v[102:105], v111 offset0:96 offset1:100
	s_waitcnt lgkmcnt(1)
	v_mfma_f32_16x16x32_bf16 v[98:101], v[98:101], v[42:45], v[114:117]
	v_fma_f32 v38, v38, s71, -v77
	v_mul_f32_e32 v38, 0x3fb8aa3b, v38
	v_fma_f32 v18, v18, s71, -v77
	s_waitcnt lgkmcnt(0)
	v_mfma_f32_16x16x32_bf16 v[42:45], v[102:105], v[42:45], v[106:109]
	v_mul_f32_e32 v18, 0x3fb8aa3b, v18
	v_fma_f32 v10, v10, s71, -v77
	v_mul_f32_e32 v10, 0x3fb8aa3b, v10
	v_exp_f32_e32 v107, v26
	v_fma_f32 v26, v35, s71, -v77
	v_mul_f32_e32 v26, 0x3fb8aa3b, v26
	v_exp_f32_e32 v108, v26
	v_fma_f32 v26, v27, s71, -v77
	v_mul_f32_e32 v26, 0x3fb8aa3b, v26
	v_exp_f32_e32 v109, v26
	v_fma_f32 v26, v36, s71, -v77
	v_mul_f32_e32 v26, 0x3fb8aa3b, v26
	v_exp_f32_e32 v112, v26
	v_fma_f32 v26, v28, s71, -v77
	v_mul_f32_e32 v26, 0x3fb8aa3b, v26
	v_exp_f32_e32 v106, v34
	v_exp_f32_e32 v113, v26
	v_fma_f32 v26, v37, s71, -v77
	ds_read2_b64 v[34:37], v124 offset0:8 offset1:12
	v_mul_f32_e32 v26, 0x3fb8aa3b, v26
	v_exp_f32_e32 v114, v26
	v_fma_f32 v26, v29, s71, -v77
	v_mul_f32_e32 v26, 0x3fb8aa3b, v26
	v_exp_f32_e32 v115, v26
	v_cvt_pk_bf16_f32 v26, v106, v108
	v_cvt_pk_bf16_f32 v27, v112, v114
	v_cvt_pk_bf16_f32 v28, v107, v109
	v_cvt_pk_bf16_f32 v29, v113, v115
	v_fma_f32 v2, v2, s71, -v77
	v_mul_f32_e32 v2, 0x3fb8aa3b, v2
	s_waitcnt lgkmcnt(0)
	v_mfma_f32_16x16x32_bf16 v[34:37], v[34:37], v[26:29], v[46:49]
	v_fma_f32 v6, v6, s71, -v77
	v_mul_f32_e32 v6, 0x3fb8aa3b, v6
	s_nop 0
	ds_read2_b64 v[46:49], v136 offset0:40 offset1:44
	s_waitcnt lgkmcnt(0)
	v_mfma_f32_16x16x32_bf16 v[46:49], v[46:49], v[26:29], v[94:97]
	s_nop 2
	ds_read2_b64 v[94:97], v110 offset0:72 offset1:76
	s_waitcnt lgkmcnt(0)
	v_mfma_f32_16x16x32_bf16 v[94:97], v[94:97], v[26:29], v[98:101]
	s_nop 2
	ds_read2_b64 v[98:101], v111 offset0:104 offset1:108
	global_load_dwordx4 v[102:105], v[78:79], off offset:384
	s_nop 0
	global_load_dwordx4 v[78:81], v[80:81], off offset:384
	s_waitcnt vmcnt(5)
	ds_write_b128 v73, v[126:129]
	s_waitcnt vmcnt(4)
	ds_write_b128 v73, v[130:133] offset:9216
	s_waitcnt lgkmcnt(2)
	v_mfma_f32_16x16x32_bf16 v[26:29], v[98:101], v[26:29], v[42:45]
	v_exp_f32_e32 v99, v30
	v_fma_f32 v30, v39, s71, -v77
	v_mul_f32_e32 v30, 0x3fb8aa3b, v30
	v_exp_f32_e32 v100, v30
	v_fma_f32 v30, v31, s71, -v77
	v_mul_f32_e32 v30, 0x3fb8aa3b, v30
	v_exp_f32_e32 v101, v30
	v_fma_f32 v30, v40, s71, -v77
	v_mul_f32_e32 v30, 0x3fb8aa3b, v30
	v_exp_f32_e32 v116, v30
	v_fma_f32 v30, v32, s71, -v77
	v_mul_f32_e32 v30, 0x3fb8aa3b, v30
	s_waitcnt lgkmcnt(0)
	s_barrier
	v_exp_f32_e32 v98, v38
	v_exp_f32_e32 v117, v30
	v_fma_f32 v30, v41, s71, -v77
	ds_read2_b64 v[38:41], v68 offset1:4
	v_mul_f32_e32 v30, 0x3fb8aa3b, v30
	v_exp_f32_e32 v126, v30
	v_fma_f32 v30, v33, s71, -v77
	v_mul_f32_e32 v30, 0x3fb8aa3b, v30
	v_exp_f32_e32 v127, v30
	v_cvt_pk_bf16_f32 v30, v98, v100
	v_cvt_pk_bf16_f32 v31, v116, v126
	v_cvt_pk_bf16_f32 v32, v99, v101
	v_cvt_pk_bf16_f32 v33, v117, v127
	ds_read2_b64 v[42:45], v90 offset0:64 offset1:68
	s_waitcnt lgkmcnt(1)
	v_mfma_f32_16x16x32_bf16 v[34:37], v[38:41], v[30:33], v[34:37]
	ds_read2_b64 v[38:41], v69 offset0:32 offset1:36
	s_waitcnt lgkmcnt(0)
	v_mfma_f32_16x16x32_bf16 v[38:41], v[38:41], v[30:33], v[46:49]
	s_nop 2
	ds_read2_b64 v[46:49], v134 offset0:96 offset1:100
	s_waitcnt lgkmcnt(0)
	v_mfma_f32_16x16x32_bf16 v[26:29], v[46:49], v[30:33], v[26:29]
	v_exp_f32_e32 v46, v18
	v_fma_f32 v18, v22, s71, -v77
	v_mul_f32_e32 v18, 0x3fb8aa3b, v18
	v_exp_f32_e32 v47, v18
	v_fma_f32 v18, v19, s71, -v77
	v_mul_f32_e32 v18, 0x3fb8aa3b, v18
	v_exp_f32_e32 v48, v18
	v_fma_f32 v18, v23, s71, -v77
	v_mul_f32_e32 v18, 0x3fb8aa3b, v18
	v_exp_f32_e32 v49, v18
	v_fma_f32 v18, v20, s71, -v77
	v_mul_f32_e32 v18, 0x3fb8aa3b, v18
	v_mfma_f32_16x16x32_bf16 v[42:45], v[42:45], v[30:33], v[94:97]
	ds_read2_b64 v[30:33], v69 offset0:40 offset1:44
	s_nop 1
	v_exp_f32_e32 v94, v18
	v_fma_f32 v18, v24, s71, -v77
	v_mul_f32_e32 v18, 0x3fb8aa3b, v18
	v_exp_f32_e32 v95, v18
	v_fma_f32 v18, v21, s71, -v77
	v_mul_f32_e32 v22, 0x3fb8aa3b, v18
	ds_read2_b64 v[18:21], v68 offset0:8 offset1:12
	v_exp_f32_e32 v68, v22
	v_fma_f32 v22, v25, s71, -v77
	v_mul_f32_e32 v22, 0x3fb8aa3b, v22
	v_exp_f32_e32 v96, v22
	v_cvt_pk_bf16_f32 v22, v46, v48
	v_cvt_pk_bf16_f32 v23, v94, v68
	v_cvt_pk_bf16_f32 v24, v47, v49
	v_cvt_pk_bf16_f32 v25, v95, v96
	s_waitcnt lgkmcnt(0)
	s_nop 0
	v_mfma_f32_16x16x32_bf16 v[18:21], v[18:21], v[22:25], v[34:37]
	v_mfma_f32_16x16x32_bf16 v[30:33], v[30:33], v[22:25], v[38:41]
	s_nop 1
	ds_read2_b64 v[34:37], v90 offset0:72 offset1:76
	ds_read2_b64 v[38:41], v134 offset0:104 offset1:108
	s_waitcnt lgkmcnt(1)
	v_mfma_f32_16x16x32_bf16 v[34:37], v[34:37], v[22:25], v[42:45]
	s_waitcnt vmcnt(1)
	ds_write_b128 v73, v[102:105] offset:18432
	s_waitcnt vmcnt(0)
	ds_write_b128 v73, v[78:81] offset:27648
	s_waitcnt lgkmcnt(0)
	s_barrier
; #define LAS __attribute__((address_space(3)))
; __device__ __forceinline__ unsigned cvt_pk_bf16(float lo, float hi) { const float __attribute__((ext_vector_type(2))) v = {lo, hi}; return __builtin_bit_cast(unsigned, __builtin_convertvector(v, bf16x2_t)); }
; #define NA_STORE(sidx) do { LAS bf16* d_ = buf + ((sidx) & 1) * 9216; _Pragma("unroll") for (int q_ = 0; q_ < 2; ++q_) *(LAS v4u*)(d_ + q_ * 4608 + lrow * 72 + lseg * 8) = ld[(sidx) & 1][q_]; } while (0)
; template <bool LOCAL>
; __device__ __forceinline__ void na_unit(const bf16* P, const bf16* VT, bf16* YCAT, const LAS float* rpb_l, LAS bf16* buf, int b, int gr, int hp, int qblk, int tid) {
;     ...
;                 const int cc = c - NLOC;
; #pragma unroll
;                 for (int p2 = 0; p2 < 2; ++p2) {
;                     float p[8];
; #pragma unroll
;                     for (int e = 0; e < 4; ++e) { p[e] = __expf(sc[4 * (cc >= 0 ? cc : 0) + 2 * p2][e] - m); p[4 + e] = __expf(sc[4 * (cc >= 0 ? cc : 0) + 2 * p2 + 1][e] - m); }
; #pragma unroll
;                     for (int e = 0; e < 8; ++e) lsum += p[e];
;                     const bf16x8 pf = __builtin_bit_cast(bf16x8, (v4u){pg8::cvt_pk_bf16(p[0], p[1]), pg8::cvt_pk_bf16(p[2], p[3]), pg8::cvt_pk_bf16(p[4], p[5]), pg8::cvt_pk_bf16(p[6], p[7])});
; #pragma unroll
;                     for (int dt = 0; dt < 4; ++dt) { const LAS bf16* vp = cb + (16 * dt + fr) * 72 + 32 * p2 + 4 * fq;
;                         o[dt] = __builtin_amdgcn_mfma_f32_16x16x32_bf16(frag44(vp, vp + 16), pf, o[dt], 0, 0, 0); }
;                 }
;             }
;         }
;         if (sidx + 1 < 2 * NCH) NA_STORE(sidx + 1);
;         __syncthreads();
;     }
;     ...
;     lsum += __shfl_xor(lsum, 16); lsum += __shfl_xor(lsum, 32);
;     const float inv = 1.f / lsum;
;     bf16* op = YCAT + (size_t)(qrow0 + fr) * D + 512 + h * 64 + 4 * fq;
; #pragma unroll
;     for (int dt = 0; dt < 4; ++dt) { v2u w; w.x = pg8::cvt_pk_bf16(o[dt][0] * inv, o[dt][1] * inv); w.y = pg8::cvt_pk_bf16(o[dt][2] * inv, o[dt][3] * inv); *(v2u*)(op + dt * 16) = w; }
	v_mfma_f32_16x16x32_bf16 v[22:25], v[38:41], v[22:25], v[26:29]
	v_exp_f32_e32 v38, v10
	v_fma_f32 v10, v14, s71, -v77
	v_mul_f32_e32 v10, 0x3fb8aa3b, v10
	v_exp_f32_e32 v39, v10
	v_fma_f32 v10, v11, s71, -v77
	v_mul_f32_e32 v10, 0x3fb8aa3b, v10
	v_exp_f32_e32 v40, v10
	v_fma_f32 v10, v15, s71, -v77
	v_mul_f32_e32 v10, 0x3fb8aa3b, v10
	v_exp_f32_e32 v41, v10
	v_fma_f32 v10, v12, s71, -v77
	v_mul_f32_e32 v10, 0x3fb8aa3b, v10
	v_exp_f32_e32 v42, v10
	v_fma_f32 v10, v16, s71, -v77
	v_mul_f32_e32 v10, 0x3fb8aa3b, v10
	v_exp_f32_e32 v43, v10
	v_fma_f32 v10, v13, s71, -v77
	ds_read2_b64 v[26:29], v110 offset0:64 offset1:68
	v_mul_f32_e32 v14, 0x3fb8aa3b, v10
	v_exp_f32_e32 v44, v14
	v_fma_f32 v14, v17, s71, -v77
	v_mul_f32_e32 v14, 0x3fb8aa3b, v14
	v_exp_f32_e32 v45, v14
	v_cvt_pk_bf16_f32 v14, v38, v40
	v_cvt_pk_bf16_f32 v15, v42, v44
	v_cvt_pk_bf16_f32 v16, v39, v41
	v_cvt_pk_bf16_f32 v17, v43, v45
	ds_read2_b64 v[10:13], v124 offset1:4
	v_mov_b32_e32 v73, v71
	s_waitcnt lgkmcnt(1)
	v_mfma_f32_16x16x32_bf16 v[26:29], v[26:29], v[14:17], v[34:37]
	s_nop 2
	v_add_f32_e32 v34, 0, v53
	v_add_f32_e32 v34, v63, v34
	v_add_f32_e32 v34, v66, v34
	v_add_f32_e32 v34, v67, v34
	v_add_f32_e32 v34, v52, v34
	v_add_f32_e32 v34, v62, v34
	v_add_f32_e32 v34, v64, v34
	v_add_f32_e32 v34, v65, v34
	v_add_f32_e32 v34, v58, v34
	v_add_f32_e32 v34, v59, v34
	v_add_f32_e32 v34, v60, v34
	v_add_f32_e32 v34, v61, v34
	v_add_f32_e32 v34, v54, v34
	v_add_f32_e32 v34, v55, v34
	v_add_f32_e32 v34, v56, v34
	v_add_f32_e32 v34, v57, v34
	s_waitcnt lgkmcnt(0)
	v_mfma_f32_16x16x32_bf16 v[10:13], v[10:13], v[14:17], v[18:21]
	v_add_f32_e32 v34, v118, v34
	v_add_f32_e32 v34, v120, v34
	v_add_f32_e32 v34, v122, v34
	ds_read2_b64 v[18:21], v136 offset0:32 offset1:36
	v_add_f32_e32 v34, v125, v34
	v_add_f32_e32 v34, v119, v34
	v_add_f32_e32 v34, v121, v34
	v_add_f32_e32 v34, v123, v34
	v_add_f32_e32 v34, v135, v34
	v_add_f32_e32 v34, v106, v34
	s_waitcnt lgkmcnt(0)
	v_mfma_f32_16x16x32_bf16 v[18:21], v[18:21], v[14:17], v[30:33]
	v_add_f32_e32 v34, v108, v34
	s_nop 1
	ds_read2_b64 v[30:33], v111 offset0:96 offset1:100
	v_add_f32_e32 v34, v112, v34
	v_add_f32_e32 v34, v114, v34
	v_add_f32_e32 v34, v107, v34
	v_add_f32_e32 v34, v109, v34
	v_add_f32_e32 v34, v113, v34
	v_add_f32_e32 v34, v115, v34
	v_add_f32_e32 v34, v98, v34
	v_add_f32_e32 v34, v100, v34
	s_waitcnt lgkmcnt(0)
	v_mfma_f32_16x16x32_bf16 v[14:17], v[30:33], v[14:17], v[22:25]
	v_add_f32_e32 v34, v116, v34
	v_add_f32_e32 v34, v126, v34
	v_add_f32_e32 v34, v99, v34
	v_exp_f32_e32 v23, v2
	v_fma_f32 v2, v7, s71, -v77
	v_mul_f32_e32 v2, 0x3fb8aa3b, v2
	v_exp_f32_e32 v24, v2
	v_fma_f32 v2, v3, s71, -v77
	v_mul_f32_e32 v2, 0x3fb8aa3b, v2
	v_add_f32_e32 v34, v101, v34
	v_exp_f32_e32 v25, v2
	v_fma_f32 v2, v8, s71, -v77
	v_add_f32_e32 v34, v117, v34
	v_mul_f32_e32 v2, 0x3fb8aa3b, v2
	v_add_f32_e32 v34, v127, v34
	v_exp_f32_e32 v30, v2
	v_fma_f32 v2, v4, s71, -v77
	v_add_f32_e32 v34, v46, v34
	v_mul_f32_e32 v2, 0x3fb8aa3b, v2
	v_add_f32_e32 v34, v48, v34
	v_exp_f32_e32 v22, v6
	v_exp_f32_e32 v31, v2
	v_fma_f32 v2, v9, s71, -v77
	ds_read2_b64 v[6:9], v124 offset0:8 offset1:12
	v_add_f32_e32 v34, v94, v34
	v_mul_f32_e32 v2, 0x3fb8aa3b, v2
	v_add_f32_e32 v34, v68, v34
	v_exp_f32_e32 v32, v2
	v_fma_f32 v2, v5, s71, -v77
	v_add_f32_e32 v34, v47, v34
	v_mul_f32_e32 v2, 0x3fb8aa3b, v2
	v_add_f32_e32 v34, v49, v34
	v_exp_f32_e32 v33, v2
	v_add_f32_e32 v34, v95, v34
	v_add_f32_e32 v34, v96, v34
	v_add_f32_e32 v34, v38, v34
	v_add_f32_e32 v34, v40, v34
	v_cvt_pk_bf16_f32 v2, v22, v24
	v_cvt_pk_bf16_f32 v3, v30, v32
	v_cvt_pk_bf16_f32 v4, v23, v25
	v_cvt_pk_bf16_f32 v5, v31, v33
	v_add_f32_e32 v34, v42, v34
	v_add_f32_e32 v34, v44, v34
	s_waitcnt lgkmcnt(0)
	v_mfma_f32_16x16x32_bf16 v[6:9], v[6:9], v[2:5], v[10:13]
	v_add_f32_e32 v34, v39, v34
	v_add_f32_e32 v34, v41, v34
	v_add_f32_e32 v34, v43, v34
	ds_read2_b64 v[10:13], v136 offset0:40 offset1:44
	v_add_f32_e32 v34, v45, v34
	v_add_f32_e32 v22, v22, v34
	v_add_f32_e32 v22, v24, v22
	v_add_f32_e32 v22, v30, v22
	v_add_f32_e32 v22, v32, v22
	s_waitcnt lgkmcnt(0)
	v_mfma_f32_16x16x32_bf16 v[10:13], v[10:13], v[2:5], v[18:21]
	s_nop 2
	ds_read2_b64 v[18:21], v110 offset0:72 offset1:76
	v_add_f32_e32 v22, v23, v22
	v_add_f32_e32 v22, v25, v22
	v_add_f32_e32 v22, v31, v22
	v_add_f32_e32 v30, v33, v22
	ds_bpermute_b32 v31, v50, v30
	ds_read2_b64 v[22:25], v111 offset0:104 offset1:108
	s_waitcnt lgkmcnt(2)
	v_mfma_f32_16x16x32_bf16 v[18:21], v[18:21], v[2:5], v[26:29]
	v_mov_b32_e32 v77, v71
	s_waitcnt lgkmcnt(1)
	s_nop 0
	v_add_f32_e32 v26, v30, v31
	ds_bpermute_b32 v27, v51, v26
	s_waitcnt lgkmcnt(1)
	v_mfma_f32_16x16x32_bf16 v[14:17], v[22:25], v[2:5], v[14:17]
	s_waitcnt lgkmcnt(0)
	v_add_f32_e32 v2, v26, v27
	v_div_scale_f32 v3, s[0:1], v2, v2, 1.0
	v_rcp_f32_e32 v4, v3
	s_barrier
	s_mov_b64 s[0:1], 0
	v_fma_f32 v5, -v3, v4, 1.0
	v_fmac_f32_e32 v4, v5, v4
	v_div_scale_f32 v5, vcc, 1.0, v2, 1.0
	v_mul_f32_e32 v22, v5, v4
	v_fma_f32 v23, -v3, v22, v5
	v_fmac_f32_e32 v22, v23, v4
	v_fma_f32 v3, -v3, v22, v5
	v_div_fmas_f32 v3, v3, v4, v22
	v_div_fixup_f32 v22, v3, v2, 1.0
	v_lshlrev_b64 v[2:3], 11, v[72:73]
	v_lshl_add_u64 v[2:3], s[10:11], 0, v[2:3]
	v_lshl_add_u64 v[2:3], v[2:3], 0, v[74:75]
	v_pk_mul_f32 v[6:7], v[6:7], v[22:23] op_sel_hi:[1,0]
	v_pk_mul_f32 v[8:9], v[8:9], v[22:23] op_sel_hi:[1,0]
	v_lshl_add_u64 v[4:5], v[2:3], 0, v[76:77]
	v_cvt_pk_bf16_f32 v6, v6, v7
	v_cvt_pk_bf16_f32 v7, v8, v9
	global_store_dwordx2 v[4:5], v[6:7], off offset:1024
	v_pk_mul_f32 v[6:7], v[10:11], v[22:23] op_sel_hi:[1,0]
	v_pk_mul_f32 v[8:9], v[12:13], v[22:23] op_sel_hi:[1,0]
	v_cvt_pk_bf16_f32 v6, v6, v7
	v_cvt_pk_bf16_f32 v7, v8, v9
	global_store_dwordx2 v[4:5], v[6:7], off offset:1056
	v_pk_mul_f32 v[6:7], v[18:19], v[22:23] op_sel_hi:[1,0]
	v_pk_mul_f32 v[8:9], v[20:21], v[22:23] op_sel_hi:[1,0]
	v_cvt_pk_bf16_f32 v6, v6, v7
	v_cvt_pk_bf16_f32 v7, v8, v9
	v_lshl_add_u64 v[2:3], v[4:5], 0, s[12:13]
	global_store_dwordx2 v[4:5], v[6:7], off offset:1088
	v_pk_mul_f32 v[4:5], v[14:15], v[22:23] op_sel_hi:[1,0]
	v_pk_mul_f32 v[6:7], v[16:17], v[22:23] op_sel_hi:[1,0]
	v_cvt_pk_bf16_f32 v4, v4, v5

; #define LAS __attribute__((address_space(3)))
; template <bool LOCAL>
; __device__ __forceinline__ void na_unit(const bf16* P, const bf16* VT, bf16* YCAT, const LAS float* rpb_l, LAS bf16* buf, int b, int gr, int hp, int qblk, int tid) {
;     ...
;     const int lane = tid & 63, wv = tid >> 6, fr = lane & 15, fq = lane >> 4, hh = wv >> 2, qb = wv & 3, h = 2 * hp + hh;
;     const int qrow0 = LOCAL ? NCTX + b * SEQ + gr * 64 + 16 * qb : b * CTXL + qblk * 64 + 16 * qb;
;     const int r0 = min(max(gr - 4, 0), 24);
;     const int kc0 = qb == 0 ? 0 : qb == 1 ? 8 : qb == 2 ? 24 : 32;
;     const int qcol = 16 * qb + fr, cs = min(max(qcol - 8, 0), 48);
;     const LAS float* rpb = rpb_l + h * 15 * 31;
;     v4u ld[2][2];
;     const int lrow = (tid >> 3) & 63, lseg = tid & 7;
;     ...
;     bf16x8 qf[2];
; #pragma unroll
;     for (int ks = 0; ks < 2; ++ks) qf[ks] = *(const bf16x8*)(P + (size_t)(qrow0 + fr) * DINP + h * 64 + 32 * ks + 8 * fq);
;     f32x4 sl[16], sc[16];
;     float m = -1.0e30f, lsum = 0.f;
;     f32x4 o[4];
; #pragma unroll
;     for (int dt = 0; dt < 4; ++dt) o[dt] = (f32x4){0.f, 0.f, 0.f, 0.f};
;     NA_ISSUE(0); NA_ISSUE(1); NA_STORE(0);
;     __syncthreads();
; #pragma unroll
;     for (int sidx = 0; sidx < 2 * NCH; ++sidx) {
;         if (sidx + 2 < 2 * NCH) NA_ISSUE(sidx + 2);
;         const LAS bf16* cb = buf + (sidx & 1) * 9216 + hh * 4608;
;         if (sidx < NCH) {
;             const int c = sidx;
;             if (LOCAL && c < 8) {
; #pragma unroll
;                 for (int t2 = 0; t2 < 2; ++t2) {
;                     const LAS bf16* kp = cb + (kc0 + 16 * t2 + fr) * 72 + 8 * fq;
;                     f32x4 acc = {0.f, 0.f, 0.f, 0.f};
;                     acc = __builtin_amdgcn_mfma_f32_16x16x32_bf16(*(const LAS bf16x8*)(kp), qf[0], acc, 0, 0, 0);
;                     acc = __builtin_amdgcn_mfma_f32_16x16x32_bf16(*(const LAS bf16x8*)(kp + 32), qf[1], acc, 0, 0, 0);
;                     const LAS float* rb = rpb + (r0 + c - gr + 7) * 31 + 15 - qcol;
; #pragma unroll
;                     for (int e = 0; e < 4; ++e) { const int kcol = kc0 + 16 * t2 + 4 * fq + e; const bool ok = (kcol >= cs) && (kcol < cs + 16);
;                         const float sv = ok ? acc[e] * 0.125f + rb[ok ? kcol : qcol] : -1.0e30f; acc[e] = sv; m = fmaxf(m, sv); }
;                     sl[2 * (c < 8 ? c : 0) + t2] = acc; }
.LBB0_1507:
	s_or_b64 exec, exec, s[0:1]
	s_bfe_u32 s19, s76, 0x50002
	v_sub_u32_e64 v3, s19, 4 clamp
	s_ashr_i32 s17, s76, 7
	v_readfirstlane_b32 s0, v3
	s_lshl_b32 s26, s17, 11
	s_min_u32 s20, s0, 24
	s_add_i32 s14, s26, 0x1000
	s_lshl_b32 s15, s20, 6
	s_or_b32 s16, s15, s14
	v_mov_b64_e32 v[18:19], s[8:9]
	v_and_b32_e32 v32, 7, v93
	v_or_b32_e32 v3, s16, v88
	s_and_b32 s18, s76, 3
	v_mad_i64_i32 v[4:5], s[0:1], v3, s69, v[18:19]
	v_lshlrev_b32_e32 v26, 4, v32
	v_mov_b32_e32 v27, v71
	v_lshl_add_u64 v[4:5], v[4:5], 0, v[26:27]
	s_lshl_b32 s2, s18, 8
	v_lshl_add_u64 v[4:5], v[4:5], 0, s[2:3]
	global_load_dwordx4 v[10:13], v[4:5], off offset:1024
	global_load_dwordx4 v[14:17], v[4:5], off offset:1152
	s_lshl_b32 s0, s19, 6
	v_lshl_or_b32 v31, v2, 4, v89
	v_lshl_add_u32 v33, s18, 1, v92
	s_or_b32 s0, s14, s0
	v_mad_u32_u24 v2, v88, s70, 0
	v_lshlrev_b32_e32 v72, 6, v33
	s_add_i32 s50, s26, 0x1040
	v_or_b32_e32 v74, s0, v31
	v_add_u32_e32 v75, v2, v26
	v_ashrrev_i32_e32 v73, 31, v72
	v_or_b32_e32 v4, s50, v88
	v_mad_i64_i32 v[2:3], s[0:1], v74, s69, v[18:19]
	v_add_u32_e32 v4, s15, v4
	v_lshl_add_u64 v[2:3], v[72:73], 1, v[2:3]
	v_mad_i64_i32 v[4:5], s[0:1], v4, s69, v[18:19]
	v_lshl_add_u64 v[2:3], v[2:3], 0, v[70:71]
	v_lshl_add_u64 v[20:21], v[4:5], 0, v[26:27]
	global_load_dwordx4 v[6:9], v[2:3], off
	s_nop 0
	global_load_dwordx4 v[2:5], v[2:3], off offset:64
	s_or_b32 s14, s26, s15
	s_addk_i32 s14, 0x1080
	v_or_b32_e32 v24, s14, v88
	v_mad_i64_i32 v[28:29], s[0:1], v24, s69, v[18:19]
	v_lshl_add_u64 v[26:27], v[28:29], 0, v[26:27]
	v_lshl_add_u64 v[22:23], v[20:21], 0, s[2:3]
	v_lshl_add_u64 v[26:27], v[26:27], 0, s[2:3]
	s_mov_b32 s100, 0x60000
	s_mov_b32 s101, 0
	v_lshl_add_u64 v[248:249], v[22:23], 0, s[100:101]
	global_load_dwordx4 v[18:21], v[22:23], off offset:1024
	s_nop 0
	global_load_dwordx4 v[22:25], v[22:23], off offset:1152
	global_load_dword v250, v[248:249], off offset:1024
	global_load_dword v251, v[248:249], off offset:1152
	v_add_u32_e32 v30, v86, v70
	v_add_u32_e32 v34, v90, v89
	v_mad_u32_u24 v36, v34, s70, v30
	s_movk_i32 s0, 0x744
	v_mul_lo_u32 v33, v33, s0
	s_sub_i32 s0, s20, s19
	s_mulk_i32 s0, 0x7c
	v_sub_u32_e64 v35, v31, 8 clamp
	s_add_i32 s0, s0, 0
	v_min_u32_e32 v35, 48, v35
	v_lshlrev_b32_e32 v77, 2, v91
	v_add_u32_e32 v33, s0, v33
	v_lshlrev_b32_e32 v31, 2, v31
	v_sub_u32_e32 v31, v33, v31
	v_add_u32_e32 v33, v90, v77
	v_cmp_ge_u32_e32 vcc, v33, v35
	v_mov_b32_e32 v91, 0xf149f2ca
	v_lshl_add_u32 v31, v33, 2, v31
	v_mov_b32_e32 v92, 0xf149f2ca
	s_waitcnt vmcnt(7)
	ds_write_b128 v75, v[10:13]
	s_waitcnt vmcnt(6)
	ds_write_b128 v75, v[14:17] offset:9216
	s_waitcnt lgkmcnt(0)
	s_barrier
	ds_read_b32 v240, v31 offset:37792
	ds_read_b32 v241, v31 offset:37796
	ds_read_b32 v242, v31 offset:37800
	ds_read_b32 v243, v31 offset:37804
	ds_read_b32 v244, v31 offset:37856
	ds_read_b32 v245, v31 offset:37860
	ds_read_b32 v246, v31 offset:37864
	ds_read_b32 v247, v31 offset:37868
	v_lshl_add_u64 v[248:249], v[26:27], 0, s[100:101]
	global_load_dwordx4 v[10:13], v[26:27], off offset:1024
	global_load_dwordx4 v[14:17], v[26:27], off offset:1152
	global_load_dword v250, v[248:249], off offset:1024
	global_load_dword v251, v[248:249], off offset:1152
	ds_read_b128 v[26:29], v36
	ds_read_b128 v[38:41], v36 offset:64
	s_waitcnt vmcnt(9) lgkmcnt(1)
	v_mfma_f32_16x16x32_bf16 v[26:29], v[26:29], v[6:9], 0
	v_add_u32_e32 v36, 16, v35
	v_cmp_lt_u32_e64 s[0:1], v33, v36
	s_and_b64 s[28:29], vcc, s[0:1]
	s_waitcnt vmcnt(8) lgkmcnt(0)
	v_mfma_f32_16x16x32_bf16 v[26:29], v[38:41], v[2:5], v[26:29]
	s_nop 2
	s_waitcnt lgkmcnt(0)
	s_nop 3
	v_fmac_f32_e32 v240, 0x3e000000, v26
	v_cndmask_b32_e64 v92, v92, v240, s[28:29]
	s_nop 4
	v_or_b32_e32 v26, 1, v33
	v_cmp_ge_u32_e32 vcc, v26, v35
	v_cmp_lt_u32_e64 s[0:1], v26, v36
	s_and_b64 s[30:31], vcc, s[0:1]
	s_nop 2
	s_waitcnt lgkmcnt(0)
	v_fmac_f32_e32 v241, 0x3e000000, v27
	v_cndmask_b32_e64 v91, v91, v241, s[30:31]
	v_or_b32_e32 v26, 2, v33
	v_cmp_ge_u32_e32 vcc, v26, v35
	v_cmp_lt_u32_e64 s[0:1], v26, v36
	s_and_b64 s[34:35], vcc, s[0:1]
	v_mov_b32_e32 v93, 0xf149f2ca
	v_mov_b32_e32 v94, 0xf149f2ca
	s_nop 2
	s_waitcnt lgkmcnt(0)
	v_fmac_f32_e32 v242, 0x3e000000, v28
	v_cndmask_b32_e64 v94, v94, v242, s[34:35]
	v_or_b32_e32 v26, 3, v33
	v_cmp_ge_u32_e32 vcc, v26, v35
	v_cmp_lt_u32_e64 s[0:1], v26, v36
	s_and_b64 s[36:37], vcc, s[0:1]
	s_nop 2
	s_waitcnt lgkmcnt(0)
	v_fmac_f32_e32 v243, 0x3e000000, v29
	v_cndmask_b32_e64 v93, v93, v243, s[36:37]
	v_add_u32_e32 v37, 16, v90
	v_add_u32_e32 v33, v37, v89
	v_mad_u32_u24 v38, v33, s70, v30
	ds_read_b128 v[26:29], v38
	ds_read_b128 v[38:41], v38 offset:64
	v_add_u32_e32 v37, v37, v77
	v_cmp_ge_u32_e32 vcc, v37, v35
	v_cmp_lt_u32_e64 s[0:1], v37, v36
	s_waitcnt lgkmcnt(1)
	v_mfma_f32_16x16x32_bf16 v[26:29], v[26:29], v[6:9], 0
	s_and_b64 s[38:39], vcc, s[0:1]
	v_mov_b32_e32 v95, 0xf149f2ca
	v_mov_b32_e32 v96, 0xf149f2ca
	s_waitcnt lgkmcnt(0)
	v_mfma_f32_16x16x32_bf16 v[26:29], v[38:41], v[2:5], v[26:29]
	s_nop 2
	s_waitcnt lgkmcnt(0)
	s_nop 3
	v_fmac_f32_e32 v244, 0x3e000000, v26
	v_cndmask_b32_e64 v96, v96, v244, s[38:39]
	s_nop 4
	v_or_b32_e32 v26, 1, v37
	v_cmp_ge_u32_e32 vcc, v26, v35
	v_cmp_lt_u32_e64 s[0:1], v26, v36
	s_and_b64 s[44:45], vcc, s[0:1]
	s_nop 2
	s_waitcnt lgkmcnt(0)
	v_fmac_f32_e32 v245, 0x3e000000, v27
	v_cndmask_b32_e64 v95, v95, v245, s[44:45]
	v_or_b32_e32 v26, 2, v37
	v_cmp_ge_u32_e32 vcc, v26, v35
	v_cmp_lt_u32_e64 s[0:1], v26, v36
	s_and_b64 s[46:47], vcc, s[0:1]
	v_mov_b32_e32 v97, 0xf149f2ca
	v_mov_b32_e32 v99, 0xf149f2ca
	s_nop 2
	s_waitcnt lgkmcnt(0)
	v_fmac_f32_e32 v246, 0x3e000000, v28
	v_cndmask_b32_e64 v99, v99, v246, s[46:47]
	v_or_b32_e32 v26, 3, v37
	v_cmp_ge_u32_e32 vcc, v26, v35
	v_cmp_lt_u32_e64 s[0:1], v26, v36
	s_and_b64 s[48:49], vcc, s[0:1]
	s_nop 2
	s_waitcnt lgkmcnt(0)
	v_fmac_f32_e32 v247, 0x3e000000, v29
	v_cndmask_b32_e64 v97, v97, v247, s[48:49]
	v_mul_u32_u24_e32 v27, 0x90, v34
	v_lshlrev_b32_e32 v26, 3, v32
	v_add_u32_e32 v32, v30, v27
	s_waitcnt vmcnt(7)
	ds_write_b128 v75, v[18:21] offset:18432
	s_waitcnt vmcnt(6)
	ds_write_b128 v75, v[22:25] offset:27648
	s_waitcnt lgkmcnt(0)
	s_barrier
; #define LAS __attribute__((address_space(3)))
; template <bool LOCAL>
; __device__ __forceinline__ void na_unit(const bf16* P, const bf16* VT, bf16* YCAT, const LAS float* rpb_l, LAS bf16* buf, int b, int gr, int hp, int qblk, int tid) {
;     ...
;         if (sidx + 2 < 2 * NCH) NA_ISSUE(sidx + 2);
;         const LAS bf16* cb = buf + (sidx & 1) * 9216 + hh * 4608;
;         if (sidx < NCH) {
;             const int c = sidx;
;             if (LOCAL && c < 8) {
; #pragma unroll
;                 for (int t2 = 0; t2 < 2; ++t2) {
;                     const LAS bf16* kp = cb + (kc0 + 16 * t2 + fr) * 72 + 8 * fq;
;                     f32x4 acc = {0.f, 0.f, 0.f, 0.f};
;                     acc = __builtin_amdgcn_mfma_f32_16x16x32_bf16(*(const LAS bf16x8*)(kp), qf[0], acc, 0, 0, 0);
;                     acc = __builtin_amdgcn_mfma_f32_16x16x32_bf16(*(const LAS bf16x8*)(kp + 32), qf[1], acc, 0, 0, 0);
;                     const LAS float* rb = rpb + (r0 + c - gr + 7) * 31 + 15 - qcol;
; #pragma unroll
;                     for (int e = 0; e < 4; ++e) { const int kcol = kc0 + 16 * t2 + 4 * fq + e; const bool ok = (kcol >= cs) && (kcol < cs + 16);
;                         const float sv = ok ? acc[e] * 0.125f + rb[ok ? kcol : qcol] : -1.0e30f; acc[e] = sv; m = fmaxf(m, sv); }
;                     sl[2 * (c < 8 ? c : 0) + t2] = acc; }
	ds_read_b32 v240, v31 offset:37916
	ds_read_b32 v241, v31 offset:37920
	ds_read_b32 v242, v31 offset:37924
	ds_read_b32 v243, v31 offset:37928
	ds_read_b32 v244, v31 offset:37980
	ds_read_b32 v245, v31 offset:37984
	ds_read_b32 v246, v31 offset:37988
	ds_read_b32 v247, v31 offset:37992
	ds_read_b128 v[18:21], v32 offset:18432
	s_add_i32 s26, s26, s15
	s_add_i32 s0, s26, 0x10c0
	v_or_b32_e32 v24, s0, v88
	v_mov_b64_e32 v[22:23], s[8:9]
	s_lshl_b32 s1, s18, 7
	v_mad_i64_i32 v[22:23], s[18:19], v24, s69, v[22:23]
	v_lshlrev_b32_e32 v70, 1, v26
	v_lshl_add_u64 v[22:23], v[22:23], 0, v[70:71]
	s_lshl_b32 s2, s1, 1
	v_lshl_add_u64 v[22:23], v[22:23], 0, s[2:3]
	ds_read_b128 v[26:29], v32 offset:18496
	s_waitcnt lgkmcnt(1)
	v_mfma_f32_16x16x32_bf16 v[34:37], v[18:21], v[6:9], 0
	v_lshl_add_u64 v[248:249], v[22:23], 0, s[100:101]
	global_load_dwordx4 v[18:21], v[22:23], off offset:1024
	s_nop 0
	global_load_dwordx4 v[22:25], v[22:23], off offset:1152
	global_load_dword v250, v[248:249], off offset:1024
	global_load_dword v251, v[248:249], off offset:1152
	v_mov_b32_e32 v98, 0xf149f2ca
	v_mov_b32_e32 v100, 0xf149f2ca
	s_waitcnt lgkmcnt(0)
	v_mfma_f32_16x16x32_bf16 v[26:29], v[26:29], v[2:5], v[34:37]
	s_nop 2
	s_waitcnt lgkmcnt(0)
	s_nop 3
	v_fmac_f32_e32 v240, 0x3e000000, v26
	v_cndmask_b32_e64 v100, v100, v240, s[28:29]
	s_nop 2
	s_waitcnt lgkmcnt(0)
	s_nop 0
	v_fmac_f32_e32 v241, 0x3e000000, v27
	v_cndmask_b32_e64 v98, v98, v241, s[30:31]
	v_mov_b32_e32 v101, 0xf149f2ca
	v_mov_b32_e32 v102, 0xf149f2ca
	s_nop 2
	s_waitcnt lgkmcnt(0)
	v_fmac_f32_e32 v242, 0x3e000000, v28
	v_cndmask_b32_e64 v102, v102, v242, s[34:35]
	s_nop 2
	s_waitcnt lgkmcnt(0)
	v_fmac_f32_e32 v243, 0x3e000000, v29
	v_cndmask_b32_e64 v101, v101, v243, s[36:37]
	v_mul_u32_u24_e32 v26, 0x90, v33
	v_add_u32_e32 v33, v30, v26
	ds_read_b128 v[26:29], v33 offset:18432
	ds_read_b128 v[34:37], v33 offset:18496
	v_mov_b32_e32 v103, 0xf149f2ca
	v_mov_b32_e32 v105, 0xf149f2ca
	s_waitcnt lgkmcnt(1)
	v_mfma_f32_16x16x32_bf16 v[26:29], v[26:29], v[6:9], 0
	s_waitcnt lgkmcnt(0)
	v_mfma_f32_16x16x32_bf16 v[26:29], v[34:37], v[2:5], v[26:29]
	s_nop 2
	s_waitcnt lgkmcnt(0)
	s_nop 3
	v_fmac_f32_e32 v244, 0x3e000000, v26
	v_cndmask_b32_e64 v105, v105, v244, s[38:39]
	s_nop 2
	s_waitcnt lgkmcnt(0)
	s_nop 0
	v_fmac_f32_e32 v245, 0x3e000000, v27
	v_cndmask_b32_e64 v103, v103, v245, s[44:45]
	v_mov_b32_e32 v107, 0xf149f2ca
	v_mov_b32_e32 v109, 0xf149f2ca
	s_nop 2
	s_waitcnt lgkmcnt(0)
	v_fmac_f32_e32 v246, 0x3e000000, v28
	v_cndmask_b32_e64 v109, v109, v246, s[46:47]
	s_nop 2
	s_waitcnt lgkmcnt(0)
	v_fmac_f32_e32 v247, 0x3e000000, v29
	v_cndmask_b32_e64 v107, v107, v247, s[48:49]
	s_waitcnt vmcnt(7)
	ds_write_b128 v75, v[10:13]
	s_waitcnt vmcnt(6)
	ds_write_b128 v75, v[14:17] offset:9216
	s_waitcnt lgkmcnt(0)
	s_barrier
	ds_read_b32 v240, v31 offset:38040
	ds_read_b32 v241, v31 offset:38044
	ds_read_b32 v242, v31 offset:38048
	ds_read_b32 v243, v31 offset:38052
	ds_read_b32 v244, v31 offset:38104
	ds_read_b32 v245, v31 offset:38108
	ds_read_b32 v246, v31 offset:38112
	ds_read_b32 v247, v31 offset:38116
	ds_read_b128 v[10:13], v32
	ds_read_b128 v[26:29], v32 offset:64
	s_add_i32 s18, s26, 0x1100
	v_or_b32_e32 v16, s18, v88
	v_mov_b64_e32 v[14:15], s[8:9]
	v_mad_i64_i32 v[14:15], s[20:21], v16, s69, v[14:15]
	v_lshl_add_u64 v[14:15], v[14:15], 0, v[70:71]
	v_lshl_add_u64 v[14:15], v[14:15], 0, s[2:3]
	s_waitcnt lgkmcnt(1)
	v_mfma_f32_16x16x32_bf16 v[34:37], v[10:13], v[6:9], 0
	v_lshl_add_u64 v[248:249], v[14:15], 0, s[100:101]
	global_load_dwordx4 v[10:13], v[14:15], off offset:1024
	s_nop 0
	global_load_dwordx4 v[14:17], v[14:15], off offset:1152
	global_load_dword v250, v[248:249], off offset:1024
	global_load_dword v251, v[248:249], off offset:1152
	v_mov_b32_e32 v104, 0xf149f2ca
	v_mov_b32_e32 v106, 0xf149f2ca
	s_waitcnt lgkmcnt(0)
	v_mfma_f32_16x16x32_bf16 v[26:29], v[26:29], v[2:5], v[34:37]
	s_nop 2
	s_waitcnt lgkmcnt(0)
	s_nop 3
	v_fmac_f32_e32 v240, 0x3e000000, v26
	v_cndmask_b32_e64 v106, v106, v240, s[28:29]
	s_nop 2
	s_waitcnt lgkmcnt(0)
	s_nop 0
	v_fmac_f32_e32 v241, 0x3e000000, v27
	v_cndmask_b32_e64 v104, v104, v241, s[30:31]
	v_mov_b32_e32 v108, 0xf149f2ca
	v_mov_b32_e32 v110, 0xf149f2ca
	s_nop 2
	s_waitcnt lgkmcnt(0)
	v_fmac_f32_e32 v242, 0x3e000000, v28
	v_cndmask_b32_e64 v110, v110, v242, s[34:35]
	s_nop 2
	s_waitcnt lgkmcnt(0)
	v_fmac_f32_e32 v243, 0x3e000000, v29
	v_cndmask_b32_e64 v108, v108, v243, s[36:37]
	ds_read_b128 v[26:29], v33
	ds_read_b128 v[34:37], v33 offset:64
	v_mov_b32_e32 v111, 0xf149f2ca
	v_mov_b32_e32 v113, 0xf149f2ca
	s_waitcnt lgkmcnt(1)
	v_mfma_f32_16x16x32_bf16 v[26:29], v[26:29], v[6:9], 0
	s_waitcnt lgkmcnt(0)
	v_mfma_f32_16x16x32_bf16 v[26:29], v[34:37], v[2:5], v[26:29]
	s_nop 2
	s_waitcnt lgkmcnt(0)
	s_nop 3
	v_fmac_f32_e32 v244, 0x3e000000, v26
	v_cndmask_b32_e64 v113, v113, v244, s[38:39]
	s_nop 2
	s_waitcnt lgkmcnt(0)
	s_nop 0
	v_fmac_f32_e32 v245, 0x3e000000, v27
	v_cndmask_b32_e64 v111, v111, v245, s[44:45]
	v_mov_b32_e32 v112, 0xf149f2ca
	v_mov_b32_e32 v116, 0xf149f2ca
	s_nop 2
	s_waitcnt lgkmcnt(0)
	v_fmac_f32_e32 v246, 0x3e000000, v28
	v_cndmask_b32_e64 v116, v116, v246, s[46:47]
	s_nop 2
	s_waitcnt lgkmcnt(0)
	v_fmac_f32_e32 v247, 0x3e000000, v29
	v_cndmask_b32_e64 v112, v112, v247, s[48:49]
	s_waitcnt vmcnt(7)
	ds_write_b128 v75, v[18:21] offset:18432
	s_waitcnt vmcnt(6)
	ds_write_b128 v75, v[22:25] offset:27648
	s_waitcnt lgkmcnt(0)
	s_barrier
; #define LAS __attribute__((address_space(3)))
; template <bool LOCAL>
; __device__ __forceinline__ void na_unit(const bf16* P, const bf16* VT, bf16* YCAT, const LAS float* rpb_l, LAS bf16* buf, int b, int gr, int hp, int qblk, int tid) {
;     ...
;         if (sidx + 2 < 2 * NCH) NA_ISSUE(sidx + 2);
;         const LAS bf16* cb = buf + (sidx & 1) * 9216 + hh * 4608;
;         if (sidx < NCH) {
;             const int c = sidx;
;             if (LOCAL && c < 8) {
; #pragma unroll
;                 for (int t2 = 0; t2 < 2; ++t2) {
;                     const LAS bf16* kp = cb + (kc0 + 16 * t2 + fr) * 72 + 8 * fq;
;                     f32x4 acc = {0.f, 0.f, 0.f, 0.f};
;                     acc = __builtin_amdgcn_mfma_f32_16x16x32_bf16(*(const LAS bf16x8*)(kp), qf[0], acc, 0, 0, 0);
;                     acc = __builtin_amdgcn_mfma_f32_16x16x32_bf16(*(const LAS bf16x8*)(kp + 32), qf[1], acc, 0, 0, 0);
;                     const LAS float* rb = rpb + (r0 + c - gr + 7) * 31 + 15 - qcol;
; #pragma unroll
;                     for (int e = 0; e < 4; ++e) { const int kcol = kc0 + 16 * t2 + 4 * fq + e; const bool ok = (kcol >= cs) && (kcol < cs + 16);
;                         const float sv = ok ? acc[e] * 0.125f + rb[ok ? kcol : qcol] : -1.0e30f; acc[e] = sv; m = fmaxf(m, sv); }
;                     sl[2 * (c < 8 ? c : 0) + t2] = acc; }
	ds_read_b32 v240, v31 offset:38164
	ds_read_b32 v241, v31 offset:38168
	ds_read_b32 v242, v31 offset:38172
	ds_read_b32 v243, v31 offset:38176
	ds_read_b32 v244, v31 offset:38228
	ds_read_b32 v245, v31 offset:38232
	ds_read_b32 v246, v31 offset:38236
	ds_read_b32 v247, v31 offset:38240
	ds_read_b128 v[18:21], v32 offset:18432
	ds_read_b128 v[26:29], v32 offset:18496
	s_add_i32 s20, s26, 0x1140
	v_or_b32_e32 v24, s20, v88
	v_mov_b64_e32 v[22:23], s[8:9]
	v_mad_i64_i32 v[22:23], s[22:23], v24, s69, v[22:23]
	v_lshl_add_u64 v[22:23], v[22:23], 0, v[70:71]
	v_lshl_add_u64 v[22:23], v[22:23], 0, s[2:3]
	s_waitcnt lgkmcnt(1)
	v_mfma_f32_16x16x32_bf16 v[34:37], v[18:21], v[6:9], 0
	v_lshl_add_u64 v[248:249], v[22:23], 0, s[100:101]
	global_load_dwordx4 v[18:21], v[22:23], off offset:1024
	s_nop 0
	global_load_dwordx4 v[22:25], v[22:23], off offset:1152
	global_load_dword v250, v[248:249], off offset:1024
	global_load_dword v251, v[248:249], off offset:1152
	v_mov_b32_e32 v114, 0xf149f2ca
	v_mov_b32_e32 v115, 0xf149f2ca
	s_waitcnt lgkmcnt(0)
	v_mfma_f32_16x16x32_bf16 v[26:29], v[26:29], v[2:5], v[34:37]
	s_nop 2
	s_waitcnt lgkmcnt(0)
	s_nop 3
	v_fmac_f32_e32 v240, 0x3e000000, v26
	v_cndmask_b32_e64 v115, v115, v240, s[28:29]
	s_nop 2
	s_waitcnt lgkmcnt(0)
	s_nop 0
	v_fmac_f32_e32 v241, 0x3e000000, v27
	v_cndmask_b32_e64 v114, v114, v241, s[30:31]
	v_mov_b32_e32 v117, 0xf149f2ca
	v_mov_b32_e32 v118, 0xf149f2ca
	s_nop 2
	s_waitcnt lgkmcnt(0)
	v_fmac_f32_e32 v242, 0x3e000000, v28
	v_cndmask_b32_e64 v118, v118, v242, s[34:35]
	s_nop 2
	s_waitcnt lgkmcnt(0)
	v_fmac_f32_e32 v243, 0x3e000000, v29
	v_cndmask_b32_e64 v117, v117, v243, s[36:37]
	ds_read_b128 v[26:29], v33 offset:18432
	ds_read_b128 v[34:37], v33 offset:18496
	v_mov_b32_e32 v119, 0xf149f2ca
	v_mov_b32_e32 v121, 0xf149f2ca
	s_waitcnt lgkmcnt(1)
	v_mfma_f32_16x16x32_bf16 v[26:29], v[26:29], v[6:9], 0
	s_waitcnt lgkmcnt(0)
	v_mfma_f32_16x16x32_bf16 v[26:29], v[34:37], v[2:5], v[26:29]
	s_nop 2
	s_waitcnt lgkmcnt(0)
	s_nop 3
	v_fmac_f32_e32 v244, 0x3e000000, v26
	v_cndmask_b32_e64 v121, v121, v244, s[38:39]
	s_nop 2
	s_waitcnt lgkmcnt(0)
	s_nop 0
	v_fmac_f32_e32 v245, 0x3e000000, v27
	v_cndmask_b32_e64 v119, v119, v245, s[44:45]
	v_mov_b32_e32 v120, 0xf149f2ca
	v_mov_b32_e32 v124, 0xf149f2ca
	s_nop 2
	s_waitcnt lgkmcnt(0)
	v_fmac_f32_e32 v246, 0x3e000000, v28
	v_cndmask_b32_e64 v124, v124, v246, s[46:47]
	s_nop 2
	s_waitcnt lgkmcnt(0)
	v_fmac_f32_e32 v247, 0x3e000000, v29
	v_cndmask_b32_e64 v120, v120, v247, s[48:49]
	s_waitcnt vmcnt(7)
	ds_write_b128 v75, v[10:13]
	s_waitcnt vmcnt(6)
	ds_write_b128 v75, v[14:17] offset:9216
	s_waitcnt lgkmcnt(0)
	s_barrier
	ds_read_b32 v240, v31 offset:38288
	ds_read_b32 v241, v31 offset:38292
	ds_read_b32 v242, v31 offset:38296
	ds_read_b32 v243, v31 offset:38300
	ds_read_b32 v244, v31 offset:38352
	ds_read_b32 v245, v31 offset:38356
	ds_read_b32 v246, v31 offset:38360
	ds_read_b32 v247, v31 offset:38364
	ds_read_b128 v[10:13], v32
	ds_read_b128 v[26:29], v32 offset:64
	s_add_i32 s22, s26, 0x1180
	v_or_b32_e32 v16, s22, v88
	v_mov_b64_e32 v[14:15], s[8:9]
	v_mad_i64_i32 v[14:15], s[24:25], v16, s69, v[14:15]
	v_lshl_add_u64 v[14:15], v[14:15], 0, v[70:71]
	v_lshl_add_u64 v[14:15], v[14:15], 0, s[2:3]
	s_waitcnt lgkmcnt(1)
	v_mfma_f32_16x16x32_bf16 v[34:37], v[10:13], v[6:9], 0
	v_lshl_add_u64 v[248:249], v[14:15], 0, s[100:101]
	global_load_dwordx4 v[10:13], v[14:15], off offset:1024
	s_nop 0
	global_load_dwordx4 v[14:17], v[14:15], off offset:1152
	global_load_dword v250, v[248:249], off offset:1024
	global_load_dword v251, v[248:249], off offset:1152
	v_mov_b32_e32 v122, 0xf149f2ca
	v_mov_b32_e32 v123, 0xf149f2ca
	s_waitcnt lgkmcnt(0)
	v_mfma_f32_16x16x32_bf16 v[26:29], v[26:29], v[2:5], v[34:37]
	s_nop 2
	s_waitcnt lgkmcnt(0)
	s_nop 3
	v_fmac_f32_e32 v240, 0x3e000000, v26
	v_cndmask_b32_e64 v123, v123, v240, s[28:29]
	s_nop 2
	s_waitcnt lgkmcnt(0)
	s_nop 0
	v_fmac_f32_e32 v241, 0x3e000000, v27
	v_cndmask_b32_e64 v122, v122, v241, s[30:31]
	v_mov_b32_e32 v125, 0xf149f2ca
	v_mov_b32_e32 v126, 0xf149f2ca
	s_nop 2
	s_waitcnt lgkmcnt(0)
	v_fmac_f32_e32 v242, 0x3e000000, v28
	v_cndmask_b32_e64 v126, v126, v242, s[34:35]
	s_nop 2
	s_waitcnt lgkmcnt(0)
	v_fmac_f32_e32 v243, 0x3e000000, v29
	v_cndmask_b32_e64 v125, v125, v243, s[36:37]
	ds_read_b128 v[26:29], v33
	ds_read_b128 v[34:37], v33 offset:64
	v_mov_b32_e32 v127, 0xf149f2ca
	v_mov_b32_e32 v129, 0xf149f2ca
	s_waitcnt lgkmcnt(1)
	v_mfma_f32_16x16x32_bf16 v[26:29], v[26:29], v[6:9], 0
	s_waitcnt lgkmcnt(0)
	v_mfma_f32_16x16x32_bf16 v[26:29], v[34:37], v[2:5], v[26:29]
	s_nop 2
	s_waitcnt lgkmcnt(0)
	s_nop 3
	v_fmac_f32_e32 v244, 0x3e000000, v26
	v_cndmask_b32_e64 v129, v129, v244, s[38:39]
	s_nop 2
	s_waitcnt lgkmcnt(0)
	s_nop 0
	v_fmac_f32_e32 v245, 0x3e000000, v27
	v_cndmask_b32_e64 v127, v127, v245, s[44:45]
	v_mov_b32_e32 v128, 0xf149f2ca
	v_mov_b32_e32 v133, 0xf149f2ca
	s_nop 2
	s_waitcnt lgkmcnt(0)
	v_fmac_f32_e32 v246, 0x3e000000, v28
	v_cndmask_b32_e64 v133, v133, v246, s[46:47]
	s_nop 2
	s_waitcnt lgkmcnt(0)
	v_fmac_f32_e32 v247, 0x3e000000, v29
	v_cndmask_b32_e64 v128, v128, v247, s[48:49]
	s_waitcnt vmcnt(7)
	ds_write_b128 v75, v[18:21] offset:18432
	s_waitcnt vmcnt(6)
	ds_write_b128 v75, v[22:25] offset:27648
	s_waitcnt lgkmcnt(0)
	s_barrier
; #define LAS __attribute__((address_space(3)))
; template <bool LOCAL>
; __device__ __forceinline__ void na_unit(const bf16* P, const bf16* VT, bf16* YCAT, const LAS float* rpb_l, LAS bf16* buf, int b, int gr, int hp, int qblk, int tid) {
;     ...
;         if (sidx + 2 < 2 * NCH) NA_ISSUE(sidx + 2);
;         const LAS bf16* cb = buf + (sidx & 1) * 9216 + hh * 4608;
;         if (sidx < NCH) {
;             const int c = sidx;
;             if (LOCAL && c < 8) {
; #pragma unroll
;                 for (int t2 = 0; t2 < 2; ++t2) {
;                     const LAS bf16* kp = cb + (kc0 + 16 * t2 + fr) * 72 + 8 * fq;
;                     f32x4 acc = {0.f, 0.f, 0.f, 0.f};
;                     acc = __builtin_amdgcn_mfma_f32_16x16x32_bf16(*(const LAS bf16x8*)(kp), qf[0], acc, 0, 0, 0);
;                     acc = __builtin_amdgcn_mfma_f32_16x16x32_bf16(*(const LAS bf16x8*)(kp + 32), qf[1], acc, 0, 0, 0);
;                     const LAS float* rb = rpb + (r0 + c - gr + 7) * 31 + 15 - qcol;
; #pragma unroll
;                     for (int e = 0; e < 4; ++e) { const int kcol = kc0 + 16 * t2 + 4 * fq + e; const bool ok = (kcol >= cs) && (kcol < cs + 16);
;                         const float sv = ok ? acc[e] * 0.125f + rb[ok ? kcol : qcol] : -1.0e30f; acc[e] = sv; m = fmaxf(m, sv); }
;                     sl[2 * (c < 8 ? c : 0) + t2] = acc; }
	ds_read_b32 v240, v31 offset:38412
	ds_read_b32 v241, v31 offset:38416
	ds_read_b32 v242, v31 offset:38420
	ds_read_b32 v243, v31 offset:38424
	ds_read_b32 v244, v31 offset:38476
	ds_read_b32 v245, v31 offset:38480
	ds_read_b32 v246, v31 offset:38484
	ds_read_b32 v247, v31 offset:38488
	ds_read_b128 v[18:21], v32 offset:18432
	ds_read_b128 v[26:29], v32 offset:18496
	s_add_i32 s24, s26, 0x11c0
	v_or_b32_e32 v24, s24, v88
	v_mov_b64_e32 v[22:23], s[8:9]
	v_mad_i64_i32 v[22:23], s[26:27], v24, s69, v[22:23]
	v_lshl_add_u64 v[22:23], v[22:23], 0, v[70:71]
	v_lshl_add_u64 v[22:23], v[22:23], 0, s[2:3]
	s_waitcnt lgkmcnt(1)
	v_mfma_f32_16x16x32_bf16 v[34:37], v[18:21], v[6:9], 0
	global_load_dwordx4 v[18:21], v[22:23], off offset:1024
	s_nop 0
	global_load_dwordx4 v[22:25], v[22:23], off offset:1152
	v_mov_b32_e32 v130, 0xf149f2ca
	v_mov_b32_e32 v132, 0xf149f2ca
	s_waitcnt lgkmcnt(0)
	v_mfma_f32_16x16x32_bf16 v[26:29], v[26:29], v[2:5], v[34:37]
	s_nop 2
	s_waitcnt lgkmcnt(0)
	s_nop 3
	v_fmac_f32_e32 v240, 0x3e000000, v26
	v_cndmask_b32_e64 v132, v132, v240, s[28:29]
	s_nop 2
	s_waitcnt lgkmcnt(0)
	s_nop 0
	v_fmac_f32_e32 v241, 0x3e000000, v27
	v_cndmask_b32_e64 v130, v130, v241, s[30:31]
	v_mov_b32_e32 v134, 0xf149f2ca
	v_mov_b32_e32 v135, 0xf149f2ca
	s_nop 2
	s_waitcnt lgkmcnt(0)
	v_fmac_f32_e32 v242, 0x3e000000, v28
	v_cndmask_b32_e64 v135, v135, v242, s[34:35]
	s_nop 2
	s_waitcnt lgkmcnt(0)
	v_fmac_f32_e32 v243, 0x3e000000, v29
	v_cndmask_b32_e64 v134, v134, v243, s[36:37]
	ds_read_b128 v[26:29], v33 offset:18432
	ds_read_b128 v[34:37], v33 offset:18496
	v_mov_b32_e32 v137, 0xf149f2ca
	v_mov_b32_e32 v139, 0xf149f2ca
	s_waitcnt lgkmcnt(1)
	v_mfma_f32_16x16x32_bf16 v[26:29], v[26:29], v[6:9], 0
	s_waitcnt lgkmcnt(0)
	v_mfma_f32_16x16x32_bf16 v[26:29], v[34:37], v[2:5], v[26:29]
	s_nop 2
	s_waitcnt lgkmcnt(0)
	s_nop 3
	v_fmac_f32_e32 v244, 0x3e000000, v26
	v_cndmask_b32_e64 v139, v139, v244, s[38:39]
	s_nop 2
	s_waitcnt lgkmcnt(0)
	s_nop 0
	v_fmac_f32_e32 v245, 0x3e000000, v27
	v_cndmask_b32_e64 v137, v137, v245, s[44:45]
	v_mov_b32_e32 v138, 0xf149f2ca
	v_mov_b32_e32 v142, 0xf149f2ca
	s_nop 2
	s_waitcnt lgkmcnt(0)
	v_fmac_f32_e32 v246, 0x3e000000, v28
	v_cndmask_b32_e64 v142, v142, v246, s[46:47]
	s_nop 2
	s_waitcnt lgkmcnt(0)
	v_fmac_f32_e32 v247, 0x3e000000, v29
	v_cndmask_b32_e64 v138, v138, v247, s[48:49]
	s_waitcnt vmcnt(5)
	ds_write_b128 v75, v[10:13]
	s_waitcnt vmcnt(4)
	ds_write_b128 v75, v[14:17] offset:9216
	s_waitcnt lgkmcnt(0)
	s_barrier
	ds_read_b32 v240, v31 offset:38536
	ds_read_b32 v241, v31 offset:38540
	ds_read_b32 v242, v31 offset:38544
	ds_read_b32 v243, v31 offset:38548
	ds_read_b32 v244, v31 offset:38600
	ds_read_b32 v245, v31 offset:38604
	ds_read_b32 v246, v31 offset:38608
	ds_read_b32 v247, v31 offset:38612
	ds_read_b128 v[10:13], v32
	ds_read_b128 v[26:29], v32 offset:64
	s_lshl_b32 s26, s17, 8
	v_or_b32_e32 v34, s26, v88
	v_mov_b64_e32 v[14:15], s[8:9]
	v_mad_i64_i32 v[14:15], s[52:53], v34, s69, v[14:15]
	v_lshl_add_u64 v[14:15], v[14:15], 0, v[70:71]
	v_lshl_add_u64 v[14:15], v[14:15], 0, s[2:3]
	s_waitcnt lgkmcnt(1)
	v_mfma_f32_16x16x32_bf16 v[36:39], v[10:13], v[6:9], 0
	v_lshl_add_u64 v[248:249], v[14:15], 0, s[100:101]
	global_load_dwordx4 v[10:13], v[14:15], off offset:1024
	s_nop 0
	global_load_dwordx4 v[14:17], v[14:15], off offset:1152
	global_load_dword v250, v[248:249], off offset:1024
	global_load_dword v251, v[248:249], off offset:1152
	v_mov_b32_e32 v140, 0xf149f2ca
	v_mov_b32_e32 v141, 0xf149f2ca
	s_waitcnt lgkmcnt(0)
	v_mfma_f32_16x16x32_bf16 v[26:29], v[26:29], v[2:5], v[36:39]
	s_nop 2
	s_waitcnt lgkmcnt(0)
	s_nop 3
	v_fmac_f32_e32 v240, 0x3e000000, v26
	v_cndmask_b32_e64 v141, v141, v240, s[28:29]
	s_nop 2
	s_waitcnt lgkmcnt(0)
	s_nop 0
	v_fmac_f32_e32 v241, 0x3e000000, v27
	v_cndmask_b32_e64 v140, v140, v241, s[30:31]
	v_mov_b32_e32 v143, 0xf149f2ca
	v_mov_b32_e32 v144, 0xf149f2ca
	s_nop 2
	s_waitcnt lgkmcnt(0)
	v_fmac_f32_e32 v242, 0x3e000000, v28
	v_cndmask_b32_e64 v144, v144, v242, s[34:35]
	s_nop 2
	s_waitcnt lgkmcnt(0)
	v_fmac_f32_e32 v243, 0x3e000000, v29
	v_cndmask_b32_e64 v143, v143, v243, s[36:37]
	ds_read_b128 v[26:29], v33
	ds_read_b128 v[36:39], v33 offset:64
	v_mov_b32_e32 v145, 0xf149f2ca
	v_mov_b32_e32 v147, 0xf149f2ca
	s_waitcnt lgkmcnt(1)
	v_mfma_f32_16x16x32_bf16 v[26:29], v[26:29], v[6:9], 0
	s_waitcnt lgkmcnt(0)
	v_mfma_f32_16x16x32_bf16 v[26:29], v[36:39], v[2:5], v[26:29]
	s_nop 2
	s_waitcnt lgkmcnt(0)
	s_nop 3
	v_fmac_f32_e32 v244, 0x3e000000, v26
	v_cndmask_b32_e64 v147, v147, v244, s[38:39]
	s_nop 2
	s_waitcnt lgkmcnt(0)
	s_nop 0
	v_fmac_f32_e32 v245, 0x3e000000, v27
	v_cndmask_b32_e64 v145, v145, v245, s[44:45]
	v_mov_b32_e32 v146, 0xf149f2ca
	v_mov_b32_e32 v150, 0xf149f2ca
	s_nop 2
	s_waitcnt lgkmcnt(0)
	v_fmac_f32_e32 v246, 0x3e000000, v28
	v_cndmask_b32_e64 v150, v150, v246, s[46:47]
	s_nop 2
	s_waitcnt lgkmcnt(0)
	v_fmac_f32_e32 v247, 0x3e000000, v29
	v_cndmask_b32_e64 v146, v146, v247, s[48:49]
	s_waitcnt vmcnt(5)
	ds_write_b128 v75, v[18:21] offset:18432
	s_waitcnt vmcnt(4)
	ds_write_b128 v75, v[22:25] offset:27648
	s_waitcnt lgkmcnt(0)
	s_barrier
; #define LAS __attribute__((address_space(3)))
; template <bool LOCAL>
; __device__ __forceinline__ void na_unit(const bf16* P, const bf16* VT, bf16* YCAT, const LAS float* rpb_l, LAS bf16* buf, int b, int gr, int hp, int qblk, int tid) {
;     ...
;         if (sidx + 2 < 2 * NCH) NA_ISSUE(sidx + 2);
;         const LAS bf16* cb = buf + (sidx & 1) * 9216 + hh * 4608;
;         if (sidx < NCH) {
;             const int c = sidx;
;             if (LOCAL && c < 8) {
; #pragma unroll
;                 for (int t2 = 0; t2 < 2; ++t2) {
;                     const LAS bf16* kp = cb + (kc0 + 16 * t2 + fr) * 72 + 8 * fq;
;                     f32x4 acc = {0.f, 0.f, 0.f, 0.f};
;                     acc = __builtin_amdgcn_mfma_f32_16x16x32_bf16(*(const LAS bf16x8*)(kp), qf[0], acc, 0, 0, 0);
;                     acc = __builtin_amdgcn_mfma_f32_16x16x32_bf16(*(const LAS bf16x8*)(kp + 32), qf[1], acc, 0, 0, 0);
;                     const LAS float* rb = rpb + (r0 + c - gr + 7) * 31 + 15 - qcol;
; #pragma unroll
;                     for (int e = 0; e < 4; ++e) { const int kcol = kc0 + 16 * t2 + 4 * fq + e; const bool ok = (kcol >= cs) && (kcol < cs + 16);
;                         const float sv = ok ? acc[e] * 0.125f + rb[ok ? kcol : qcol] : -1.0e30f; acc[e] = sv; m = fmaxf(m, sv); }
;                     sl[2 * (c < 8 ? c : 0) + t2] = acc; }
;             } else {
;                 const int cc = c - NLOC;
; #pragma unroll
;                 for (int t4 = 0; t4 < 4; ++t4) {
;                     const LAS bf16* kp = cb + (16 * t4 + fr) * 72 + 8 * fq;
;                     f32x4 acc = {0.f, 0.f, 0.f, 0.f};
;                     acc = __builtin_amdgcn_mfma_f32_16x16x32_bf16(*(const LAS bf16x8*)(kp), qf[0], acc, 0, 0, 0);
;                     acc = __builtin_amdgcn_mfma_f32_16x16x32_bf16(*(const LAS bf16x8*)(kp + 32), qf[1], acc, 0, 0, 0);
; #pragma unroll
;                     for (int e = 0; e < 4; ++e) { acc[e] *= 0.125f; m = fmaxf(m, acc[e]); }
;                     sc[4 * (cc >= 0 ? cc : 0) + t4] = acc; }
;             }
;             if (sidx == NCH - 1) { m = fmaxf(m, __shfl_xor(m, 16)); m = fmaxf(m, __shfl_xor(m, 32)); }
	ds_read_b32 v240, v31 offset:38660
	ds_read_b32 v241, v31 offset:38664
	ds_read_b32 v242, v31 offset:38668
	ds_read_b32 v243, v31 offset:38672
	ds_read_b32 v244, v31 offset:38724
	ds_read_b32 v245, v31 offset:38728
	ds_read_b32 v246, v31 offset:38732
	ds_read_b32 v247, v31 offset:38736
	ds_read_b128 v[18:21], v32 offset:18432
	ds_read_b128 v[26:29], v32 offset:18496
	v_or_b32_e32 v24, 64, v34
	v_mov_b64_e32 v[22:23], s[8:9]
	v_mad_i64_i32 v[22:23], s[52:53], v24, s69, v[22:23]
	v_lshl_add_u64 v[22:23], v[22:23], 0, v[70:71]
	v_lshl_add_u64 v[22:23], v[22:23], 0, s[2:3]
	s_waitcnt lgkmcnt(1)
	v_mfma_f32_16x16x32_bf16 v[36:39], v[18:21], v[6:9], 0
	v_lshl_add_u64 v[248:249], v[22:23], 0, s[100:101]
	global_load_dwordx4 v[18:21], v[22:23], off offset:1024
	s_nop 0
	global_load_dwordx4 v[22:25], v[22:23], off offset:1152
	global_load_dword v250, v[248:249], off offset:1024
	global_load_dword v251, v[248:249], off offset:1152
	v_mov_b32_e32 v148, 0xf149f2ca
	v_mov_b32_e32 v149, 0xf149f2ca
	s_waitcnt lgkmcnt(0)
	v_mfma_f32_16x16x32_bf16 v[26:29], v[26:29], v[2:5], v[36:39]
	s_nop 2
	s_waitcnt lgkmcnt(0)
	s_nop 3
	v_fmac_f32_e32 v240, 0x3e000000, v26
	v_cndmask_b32_e64 v149, v149, v240, s[28:29]
	s_nop 2
	s_waitcnt lgkmcnt(0)
	s_nop 0
	v_fmac_f32_e32 v241, 0x3e000000, v27
	v_cndmask_b32_e64 v148, v148, v241, s[30:31]
	v_mov_b32_e32 v151, 0xf149f2ca
	v_mov_b32_e32 v152, 0xf149f2ca
	s_nop 2
	s_waitcnt lgkmcnt(0)
	v_fmac_f32_e32 v242, 0x3e000000, v28
	v_cndmask_b32_e64 v152, v152, v242, s[34:35]
	s_nop 2
	s_waitcnt lgkmcnt(0)
	v_fmac_f32_e32 v243, 0x3e000000, v29
	v_cndmask_b32_e64 v151, v151, v243, s[36:37]
	ds_read_b128 v[26:29], v33 offset:18432
	ds_read_b128 v[36:39], v33 offset:18496
	v_mov_b32_e32 v153, 0xf149f2ca
	v_mov_b32_e32 v155, 0xf149f2ca
	s_waitcnt lgkmcnt(1)
	v_mfma_f32_16x16x32_bf16 v[26:29], v[26:29], v[6:9], 0
	s_waitcnt lgkmcnt(0)
	v_mfma_f32_16x16x32_bf16 v[26:29], v[36:39], v[2:5], v[26:29]
	s_nop 2
	s_waitcnt lgkmcnt(0)
	s_nop 3
	v_fmac_f32_e32 v244, 0x3e000000, v26
	v_cndmask_b32_e64 v155, v155, v244, s[38:39]
	s_nop 2
	s_waitcnt lgkmcnt(0)
	s_nop 0
	v_fmac_f32_e32 v245, 0x3e000000, v27
	v_cndmask_b32_e64 v153, v153, v245, s[44:45]
	v_mov_b32_e32 v154, 0xf149f2ca
	v_mov_b32_e32 v157, 0xf149f2ca
	s_nop 2
	s_waitcnt lgkmcnt(0)
	v_fmac_f32_e32 v246, 0x3e000000, v28
	v_cndmask_b32_e64 v157, v157, v246, s[46:47]
	s_nop 2
	s_waitcnt lgkmcnt(0)
	v_fmac_f32_e32 v247, 0x3e000000, v29
	v_cndmask_b32_e64 v154, v154, v247, s[48:49]
	v_max3_f32 v26, v92, s74, v91
	v_max3_f32 v26, v26, v94, v93
	v_max3_f32 v26, v26, v96, v95
	v_max3_f32 v26, v26, v99, v97
	v_max3_f32 v26, v26, v100, v98
	v_max3_f32 v26, v26, v102, v101
	v_max3_f32 v26, v26, v105, v103
	v_max3_f32 v26, v26, v109, v107
	v_max3_f32 v26, v26, v106, v104
	v_max3_f32 v26, v26, v110, v108
	v_max3_f32 v26, v26, v113, v111
	v_max3_f32 v26, v26, v116, v112
	v_max3_f32 v26, v26, v115, v114
	v_max3_f32 v26, v26, v118, v117
	v_max3_f32 v26, v26, v121, v119
	v_max3_f32 v26, v26, v124, v120
	v_max3_f32 v26, v26, v123, v122
	v_max3_f32 v26, v26, v126, v125
	v_max3_f32 v26, v26, v129, v127
	v_max3_f32 v26, v26, v133, v128
	v_max3_f32 v26, v26, v132, v130
	v_max3_f32 v26, v26, v135, v134
	v_max3_f32 v26, v26, v139, v137
	v_max3_f32 v26, v26, v142, v138
	v_max3_f32 v26, v26, v141, v140
	v_max3_f32 v26, v26, v144, v143
	v_mad_u32_u24 v89, v89, s70, v30
	v_max3_f32 v26, v26, v147, v145
	s_waitcnt vmcnt(7)
	ds_write_b128 v75, v[10:13]
	s_waitcnt vmcnt(6)
	ds_write_b128 v75, v[14:17] offset:9216
	s_waitcnt lgkmcnt(0)
	s_barrier
	ds_read_b128 v[10:13], v89
	ds_read_b128 v[14:17], v89 offset:64
	v_max3_f32 v26, v26, v150, v146
	v_max3_f32 v26, v26, v149, v148
	v_max3_f32 v26, v26, v152, v151
	v_max3_f32 v26, v26, v155, v153
	v_max3_f32 v35, v26, v157, v154
	v_or_b32_e32 v26, 0x80, v34
	v_mov_b64_e32 v[44:45], s[8:9]
	v_mad_i64_i32 v[26:27], s[28:29], v26, s69, v[44:45]
	v_lshl_add_u64 v[26:27], v[26:27], 0, v[70:71]
	v_lshl_add_u64 v[30:31], v[26:27], 0, s[2:3]
	s_waitcnt lgkmcnt(1)
	v_mfma_f32_16x16x32_bf16 v[10:13], v[10:13], v[6:9], 0
	v_lshl_add_u64 v[248:249], v[30:31], 0, s[100:101]
	global_load_dwordx4 v[26:29], v[30:31], off offset:1024
	s_nop 0
	global_load_dwordx4 v[30:33], v[30:31], off offset:1152
	global_load_dword v250, v[248:249], off offset:1024
	global_load_dword v251, v[248:249], off offset:1152
	ds_read_b128 v[36:39], v89 offset:2304
	v_lshl_add_u64 v[78:79], s[4:5], 0, v[70:71]
	s_waitcnt lgkmcnt(1)
	v_mfma_f32_16x16x32_bf16 v[62:65], v[14:17], v[2:5], v[10:13]
	s_ashr_i32 s17, s16, 31
	v_mov_b32_e32 v81, v71
	v_cmp_lt_i32_e32 vcc, v83, v84
	ds_read_b128 v[10:13], v89 offset:2368
	v_add3_u32 v156, v86, v76, v87
	s_nop 2
	v_mul_f32_e32 v14, 0x3e000000, v62
	v_mul_f32_e32 v15, 0x3e000000, v63
	v_max3_f32 v35, v35, v14, v15
	v_mul_f32_e32 v40, 0x3e000000, v64
	s_waitcnt lgkmcnt(1)
	v_mfma_f32_16x16x32_bf16 v[14:17], v[36:39], v[6:9], 0
	v_mul_f32_e32 v36, 0x3e000000, v65
	v_max3_f32 v35, v35, v40, v36
	ds_read_b128 v[36:39], v89 offset:4608
	s_waitcnt lgkmcnt(1)
	v_mfma_f32_16x16x32_bf16 v[66:69], v[10:13], v[2:5], v[14:17]
	ds_read_b128 v[10:13], v89 offset:4672
	s_ashr_i32 s19, s18, 31
	s_ashr_i32 s21, s20, 31
	s_ashr_i32 s23, s22, 31
	s_ashr_i32 s25, s24, 31
	s_nop 2
	v_mul_f32_e32 v14, 0x3e000000, v66
	v_mul_f32_e32 v15, 0x3e000000, v67
	v_max3_f32 v35, v35, v14, v15
	s_waitcnt lgkmcnt(1)
	v_mfma_f32_16x16x32_bf16 v[14:17], v[36:39], v[6:9], 0
	v_mul_f32_e32 v40, 0x3e000000, v68
	v_mul_f32_e32 v41, 0x3e000000, v69
	v_max3_f32 v35, v35, v40, v41
	s_waitcnt lgkmcnt(0)
	v_mfma_f32_16x16x32_bf16 v[58:61], v[10:13], v[2:5], v[14:17]
	ds_read_b128 v[36:39], v89 offset:6912
	ds_read_b128 v[40:43], v89 offset:6976
	s_waitcnt vmcnt(7)
	ds_write_b128 v75, v[18:21] offset:18432
	s_waitcnt vmcnt(6)
	ds_write_b128 v75, v[22:25] offset:27648
	s_waitcnt lgkmcnt(0)
	s_nop 0
	v_mul_f32_e32 v10, 0x3e000000, v58
	v_mul_f32_e32 v11, 0x3e000000, v59
	v_max3_f32 v14, v35, v10, v11
	v_mfma_f32_16x16x32_bf16 v[10:13], v[36:39], v[6:9], 0
	v_mul_f32_e32 v15, 0x3e000000, v60
	v_mul_f32_e32 v16, 0x3e000000, v61
	v_max3_f32 v14, v14, v15, v16
	v_mfma_f32_16x16x32_bf16 v[54:57], v[40:43], v[2:5], v[10:13]
	s_barrier
; #define LAS __attribute__((address_space(3)))
; template <bool LOCAL>
; __device__ __forceinline__ void na_unit(const bf16* P, const bf16* VT, bf16* YCAT, const LAS float* rpb_l, LAS bf16* buf, int b, int gr, int hp, int qblk, int tid) {
;     ...
;         if (sidx + 2 < 2 * NCH) NA_ISSUE(sidx + 2);
;         const LAS bf16* cb = buf + (sidx & 1) * 9216 + hh * 4608;
;         if (sidx < NCH) {
;             const int c = sidx;
;             if (LOCAL && c < 8) {
; #pragma unroll
;                 for (int t2 = 0; t2 < 2; ++t2) {
;                     const LAS bf16* kp = cb + (kc0 + 16 * t2 + fr) * 72 + 8 * fq;
;                     f32x4 acc = {0.f, 0.f, 0.f, 0.f};
;                     acc = __builtin_amdgcn_mfma_f32_16x16x32_bf16(*(const LAS bf16x8*)(kp), qf[0], acc, 0, 0, 0);
;                     acc = __builtin_amdgcn_mfma_f32_16x16x32_bf16(*(const LAS bf16x8*)(kp + 32), qf[1], acc, 0, 0, 0);
;                     const LAS float* rb = rpb + (r0 + c - gr + 7) * 31 + 15 - qcol;
; #pragma unroll
;                     for (int e = 0; e < 4; ++e) { const int kcol = kc0 + 16 * t2 + 4 * fq + e; const bool ok = (kcol >= cs) && (kcol < cs + 16);
;                         const float sv = ok ? acc[e] * 0.125f + rb[ok ? kcol : qcol] : -1.0e30f; acc[e] = sv; m = fmaxf(m, sv); }
;                     sl[2 * (c < 8 ? c : 0) + t2] = acc; }
;             } else {
;                 const int cc = c - NLOC;
; #pragma unroll
;                 for (int t4 = 0; t4 < 4; ++t4) {
;                     const LAS bf16* kp = cb + (16 * t4 + fr) * 72 + 8 * fq;
;                     f32x4 acc = {0.f, 0.f, 0.f, 0.f};
;                     acc = __builtin_amdgcn_mfma_f32_16x16x32_bf16(*(const LAS bf16x8*)(kp), qf[0], acc, 0, 0, 0);
;                     acc = __builtin_amdgcn_mfma_f32_16x16x32_bf16(*(const LAS bf16x8*)(kp + 32), qf[1], acc, 0, 0, 0);
; #pragma unroll
;                     for (int e = 0; e < 4; ++e) { acc[e] *= 0.125f; m = fmaxf(m, acc[e]); }
;                     sc[4 * (cc >= 0 ? cc : 0) + t4] = acc; }
;             }
;             if (sidx == NCH - 1) { m = fmaxf(m, __shfl_xor(m, 16)); m = fmaxf(m, __shfl_xor(m, 32)); }
	v_or_b32_e32 v18, 0xc0, v34
	v_mad_i64_i32 v[18:19], s[28:29], v18, s69, v[44:45]
	v_lshl_add_u64 v[18:19], v[18:19], 0, v[70:71]
	s_nop 3
	v_mul_f32_e32 v10, 0x3e000000, v54
	v_mul_f32_e32 v11, 0x3e000000, v55
	v_max3_f32 v14, v14, v10, v11
	ds_read_b128 v[10:13], v89 offset:18432
	v_mul_f32_e32 v15, 0x3e000000, v56
	v_mul_f32_e32 v16, 0x3e000000, v57
	v_max3_f32 v35, v14, v15, v16
	ds_read_b128 v[14:17], v89 offset:18496
	v_lshl_add_u64 v[22:23], v[18:19], 0, s[2:3]
	s_waitcnt lgkmcnt(1)
	v_mfma_f32_16x16x32_bf16 v[10:13], v[10:13], v[6:9], 0
	global_load_dwordx4 v[18:21], v[22:23], off offset:1024
	global_load_dwordx4 v[158:161], v[22:23], off offset:1152
	ds_read_b128 v[22:25], v89 offset:20736
	s_ashr_i32 s27, s26, 31
	s_waitcnt lgkmcnt(1)
	v_mfma_f32_16x16x32_bf16 v[46:49], v[14:17], v[2:5], v[10:13]
	s_nop 2
	ds_read_b128 v[10:13], v89 offset:20800
	s_nop 3
	v_mul_f32_e32 v14, 0x3e000000, v46
	v_mul_f32_e32 v15, 0x3e000000, v47
	v_max3_f32 v34, v35, v14, v15
	v_mul_f32_e32 v35, 0x3e000000, v48
	s_waitcnt lgkmcnt(1)
	v_mfma_f32_16x16x32_bf16 v[14:17], v[22:25], v[6:9], 0
	v_mul_f32_e32 v22, 0x3e000000, v49
	v_max3_f32 v34, v34, v35, v22
	ds_read_b128 v[22:25], v89 offset:23040
	s_waitcnt lgkmcnt(1)
	v_mfma_f32_16x16x32_bf16 v[50:53], v[10:13], v[2:5], v[14:17]
	ds_read_b128 v[10:13], v89 offset:23104
	s_nop 6
	v_mul_f32_e32 v14, 0x3e000000, v50
	v_mul_f32_e32 v15, 0x3e000000, v51
	v_max3_f32 v34, v34, v14, v15
	s_waitcnt lgkmcnt(1)
	v_mfma_f32_16x16x32_bf16 v[14:17], v[22:25], v[6:9], 0
	v_mul_f32_e32 v35, 0x3e000000, v52
	v_mul_f32_e32 v36, 0x3e000000, v53
	v_max3_f32 v38, v34, v35, v36
	s_waitcnt lgkmcnt(0)
	v_mfma_f32_16x16x32_bf16 v[42:45], v[10:13], v[2:5], v[14:17]
	ds_read_b128 v[22:25], v89 offset:25344
	ds_read_b128 v[34:37], v89 offset:25408
	s_waitcnt vmcnt(5)
	ds_write_b128 v75, v[26:29]
	s_waitcnt vmcnt(4)
	ds_write_b128 v75, v[30:33] offset:9216
	s_waitcnt lgkmcnt(0)
	s_nop 0
	v_mul_f32_e32 v10, 0x3e000000, v42
	v_mul_f32_e32 v11, 0x3e000000, v43
	v_max3_f32 v14, v38, v10, v11
	v_mfma_f32_16x16x32_bf16 v[10:13], v[22:25], v[6:9], 0
	v_mul_f32_e32 v15, 0x3e000000, v44
	v_mul_f32_e32 v16, 0x3e000000, v45
	v_max3_f32 v14, v14, v15, v16
	v_mfma_f32_16x16x32_bf16 v[38:41], v[34:37], v[2:5], v[10:13]
	s_barrier
	v_add3_u32 v26, v88, s1, 64
	v_mul_u32_u24_e32 v26, 0x9000, v26
	v_lshl_add_u64 v[22:23], s[16:17], 1, v[78:79]
	s_nop 3
	v_mul_f32_e32 v10, 0x3e000000, v38
	v_mul_f32_e32 v11, 0x3e000000, v39
	v_max3_f32 v10, v14, v10, v11
	v_mul_f32_e32 v11, 0x3e000000, v40
	v_mul_f32_e32 v12, 0x3e000000, v41
	v_max3_f32 v34, v10, v11, v12
	v_or_b32_e32 v10, s1, v88
	v_mul_u32_u24_e32 v14, 0x9000, v10
	ds_read_b128 v[10:13], v89
	v_lshlrev_b32_e32 v70, 1, v14
	ds_read_b128 v[14:17], v89 offset:64
	v_lshlrev_b32_e32 v80, 1, v26
	v_lshl_add_u64 v[24:25], v[22:23], 0, v[70:71]
	v_lshl_add_u64 v[22:23], v[22:23], 0, v[80:81]
	s_waitcnt lgkmcnt(1)
	v_mfma_f32_16x16x32_bf16 v[10:13], v[10:13], v[6:9], 0
	v_lshl_add_u64 v[248:249], v[24:25], 0, 0
	v_lshl_add_u64 v[238:239], v[22:23], 0, 0
	global_load_dwordx4 v[162:165], v[24:25], off
	global_load_dwordx4 v[166:169], v[22:23], off
	global_load_dword v250, v[248:249], off offset:128
	global_load_dword v251, v[238:239], off offset:128
	ds_read_b128 v[22:25], v89 offset:2304
	s_add_i32 s16, s15, s50
	s_waitcnt lgkmcnt(1)
	v_mfma_f32_16x16x32_bf16 v[30:33], v[14:17], v[2:5], v[10:13]
	s_ashr_i32 s17, s16, 31
	s_ashr_i32 s15, s14, 31
	v_lshl_add_u64 v[86:87], s[14:15], 1, v[78:79]
	ds_read_b128 v[10:13], v89 offset:2368
	s_ashr_i32 s1, s0, 31
	s_nop 2
	v_mul_f32_e32 v14, 0x3e000000, v30
	v_mul_f32_e32 v15, 0x3e000000, v31
	v_max3_f32 v26, v34, v14, v15
	v_mul_f32_e32 v27, 0x3e000000, v32
	s_waitcnt lgkmcnt(1)
	v_mfma_f32_16x16x32_bf16 v[14:17], v[22:25], v[6:9], 0
	v_mul_f32_e32 v22, 0x3e000000, v33
	v_max3_f32 v26, v26, v27, v22
	ds_read_b128 v[22:25], v89 offset:4608
	s_waitcnt lgkmcnt(1)
	v_mfma_f32_16x16x32_bf16 v[34:37], v[10:13], v[2:5], v[14:17]
	ds_read_b128 v[10:13], v89 offset:4672
	s_nop 6
	v_mul_f32_e32 v14, 0x3e000000, v34
	v_mul_f32_e32 v15, 0x3e000000, v35
	v_max3_f32 v26, v26, v14, v15
	s_waitcnt lgkmcnt(1)
	v_mfma_f32_16x16x32_bf16 v[14:17], v[22:25], v[6:9], 0
	v_mul_f32_e32 v27, 0x3e000000, v36
	v_mul_f32_e32 v28, 0x3e000000, v37
	v_max3_f32 v88, v26, v27, v28
	s_waitcnt lgkmcnt(0)
	v_mfma_f32_16x16x32_bf16 v[26:29], v[10:13], v[2:5], v[14:17]
	ds_read_b128 v[22:25], v89 offset:6912
	ds_read_b128 v[170:173], v89 offset:6976
	s_waitcnt vmcnt(5)
	ds_write_b128 v75, v[18:21] offset:18432
	s_waitcnt vmcnt(4)
	ds_write_b128 v75, v[158:161] offset:27648
	s_waitcnt lgkmcnt(0)
	s_nop 0
	v_mul_f32_e32 v10, 0x3e000000, v26
	v_mul_f32_e32 v11, 0x3e000000, v27
	v_max3_f32 v14, v88, v10, v11
	v_mfma_f32_16x16x32_bf16 v[10:13], v[22:25], v[6:9], 0
	v_mul_f32_e32 v15, 0x3e000000, v28
	v_mul_f32_e32 v16, 0x3e000000, v29
	v_max3_f32 v14, v14, v15, v16
	v_mfma_f32_16x16x32_bf16 v[22:25], v[170:173], v[2:5], v[10:13]
	s_barrier
; #define LAS __attribute__((address_space(3)))
; __device__ __forceinline__ unsigned cvt_pk_bf16(float lo, float hi) { const float __attribute__((ext_vector_type(2))) v = {lo, hi}; return __builtin_bit_cast(unsigned, __builtin_convertvector(v, bf16x2_t)); }
; template <bool LOCAL>
; __device__ __forceinline__ void na_unit(const bf16* P, const bf16* VT, bf16* YCAT, const LAS float* rpb_l, LAS bf16* buf, int b, int gr, int hp, int qblk, int tid) {
;     ...
;             if (sidx == NCH - 1) { m = fmaxf(m, __shfl_xor(m, 16)); m = fmaxf(m, __shfl_xor(m, 32)); }
;         } else {
;             const int c = sidx - NCH;
;             if (LOCAL && c < 8) {
;                 float p[8];
; #pragma unroll
;                 for (int e = 0; e < 4; ++e) { p[e] = __expf(sl[2 * (c < 8 ? c : 0)][e] - m); p[4 + e] = __expf(sl[2 * (c < 8 ? c : 0) + 1][e] - m); }
; #pragma unroll
;                 for (int e = 0; e < 8; ++e) lsum += p[e];
;                 const bf16x8 pf = __builtin_bit_cast(bf16x8, (v4u){pg8::cvt_pk_bf16(p[0], p[1]), pg8::cvt_pk_bf16(p[2], p[3]), pg8::cvt_pk_bf16(p[4], p[5]), pg8::cvt_pk_bf16(p[6], p[7])});
; #pragma unroll
;                 for (int dt = 0; dt < 4; ++dt) { const LAS bf16* vp = cb + (16 * dt + fr) * 72 + kc0 + 4 * fq;
;                     o[dt] = __builtin_amdgcn_mfma_f32_16x16x32_bf16(frag44(vp, vp + 16), pf, o[dt], 0, 0, 0); }
;             } else {
;                 const int cc = c - NLOC;
; #pragma unroll
;                 for (int p2 = 0; p2 < 2; ++p2) {
;                     float p[8];
; #pragma unroll
;                     for (int e = 0; e < 4; ++e) { p[e] = __expf(sc[4 * (cc >= 0 ? cc : 0) + 2 * p2][e] - m); p[4 + e] = __expf(sc[4 * (cc >= 0 ? cc : 0) + 2 * p2 + 1][e] - m); }
; #pragma unroll
;                     for (int e = 0; e < 8; ++e) lsum += p[e];
;                     const bf16x8 pf = __builtin_bit_cast(bf16x8, (v4u){pg8::cvt_pk_bf16(p[0], p[1]), pg8::cvt_pk_bf16(p[2], p[3]), pg8::cvt_pk_bf16(p[4], p[5]), pg8::cvt_pk_bf16(p[6], p[7])});
; #pragma unroll
;                     for (int dt = 0; dt < 4; ++dt) { const LAS bf16* vp = cb + (16 * dt + fr) * 72 + 32 * p2 + 4 * fq;
;                         o[dt] = __builtin_amdgcn_mfma_f32_16x16x32_bf16(frag44(vp, vp + 16), pf, o[dt], 0, 0, 0); }
;                 }
;             }
;         }
;         if (sidx + 1 < 2 * NCH) NA_STORE(sidx + 1);
	v_lshl_add_u64 v[18:19], s[16:17], 1, v[78:79]
	v_lshl_add_u64 v[20:21], v[18:19], 0, v[70:71]
	v_lshl_add_u64 v[18:19], v[18:19], 0, v[80:81]
	s_nop 3
	v_mul_f32_e32 v10, 0x3e000000, v22
	v_mul_f32_e32 v11, 0x3e000000, v23
	v_max3_f32 v14, v14, v10, v11
	ds_read_b128 v[10:13], v89 offset:18432
	v_mul_f32_e32 v15, 0x3e000000, v24
	v_mul_f32_e32 v16, 0x3e000000, v25
	v_max3_f32 v88, v14, v15, v16
	ds_read_b128 v[14:17], v89 offset:18496
	s_waitcnt lgkmcnt(1)
	v_mfma_f32_16x16x32_bf16 v[10:13], v[10:13], v[6:9], 0
	v_lshl_add_u64 v[248:249], v[20:21], 0, 0
	v_lshl_add_u64 v[238:239], v[18:19], 0, 0
	global_load_dwordx4 v[170:173], v[20:21], off
	global_load_dwordx4 v[174:177], v[18:19], off
	global_load_dword v250, v[248:249], off offset:128
	global_load_dword v251, v[238:239], off offset:128
	ds_read_b128 v[18:21], v89 offset:20736
	ds_read_b128 v[158:161], v89 offset:23040
	s_waitcnt lgkmcnt(2)
	v_mfma_f32_16x16x32_bf16 v[14:17], v[14:17], v[2:5], v[10:13]
	s_nop 2
	ds_read_b128 v[10:13], v89 offset:20800
	s_waitcnt lgkmcnt(2)
	v_mfma_f32_16x16x32_bf16 v[18:21], v[18:21], v[6:9], 0
	s_nop 1
	v_mul_f32_e32 v131, 0x3e000000, v14
	v_mul_f32_e32 v136, 0x3e000000, v15
	v_max3_f32 v88, v88, v131, v136
	s_waitcnt lgkmcnt(0)
	v_mfma_f32_16x16x32_bf16 v[18:21], v[10:13], v[2:5], v[18:21]
	ds_read_b128 v[10:13], v89 offset:23104
	ds_read_b128 v[178:181], v89 offset:25344
	ds_read_b128 v[182:185], v89 offset:25408
	v_mul_f32_e32 v131, 0x3e000000, v16
	v_mfma_f32_16x16x32_bf16 v[158:161], v[158:161], v[6:9], 0
	v_mul_f32_e32 v136, 0x3e000000, v17
	v_max3_f32 v88, v88, v131, v136
	s_nop 0
	v_mul_f32_e32 v131, 0x3e000000, v18
	s_waitcnt lgkmcnt(1)
	v_mfma_f32_16x16x32_bf16 v[6:9], v[178:181], v[6:9], 0
	v_mul_f32_e32 v136, 0x3e000000, v19
	v_max3_f32 v88, v88, v131, v136
	v_mul_f32_e32 v131, 0x3e000000, v20
	v_mfma_f32_16x16x32_bf16 v[10:13], v[10:13], v[2:5], v[158:161]
	v_mul_f32_e32 v136, 0x3e000000, v21
	v_max3_f32 v88, v88, v131, v136
	s_waitcnt vmcnt(7)
	ds_write_b128 v75, v[162:165]
	s_waitcnt vmcnt(6)
	ds_write_b128 v75, v[166:169] offset:9216
	s_waitcnt lgkmcnt(2)
	v_mfma_f32_16x16x32_bf16 v[2:5], v[182:185], v[2:5], v[6:9]
	v_mul_f32_e32 v89, 0x3e000000, v10
	v_mul_f32_e32 v131, 0x3e000000, v11
	v_max3_f32 v88, v88, v89, v131
	v_mul_f32_e32 v89, 0x3e000000, v12
	v_mul_f32_e32 v131, 0x3e000000, v13
	v_max3_f32 v88, v88, v89, v131
	s_nop 1
	v_mul_f32_e32 v6, 0x3e000000, v2
	v_mul_f32_e32 v7, 0x3e000000, v3
	v_max3_f32 v6, v88, v6, v7
	v_mul_f32_e32 v7, 0x3e000000, v4
	v_mul_f32_e32 v8, 0x3e000000, v5
	v_max3_f32 v6, v6, v7, v8
	v_cndmask_b32_e32 v7, v82, v83, vcc
	v_lshlrev_b32_e32 v88, 2, v7
	ds_bpermute_b32 v7, v88, v6
	v_cmp_lt_i32_e32 vcc, v85, v84
	v_lshl_add_u32 v8, v90, 1, v156
	s_waitcnt lgkmcnt(0)
	s_barrier
	v_max_f32_e32 v7, v7, v7
	v_max_f32_e32 v6, v6, v7
	v_cndmask_b32_e32 v7, v82, v85, vcc
	v_lshlrev_b32_e32 v89, 2, v7
	ds_bpermute_b32 v7, v89, v6
	s_waitcnt lgkmcnt(0)
	ds_read2_b64 v[158:161], v8 offset1:4
	v_max_f32_e32 v7, v7, v7
	v_max_f32_e32 v136, v6, v7
	v_sub_f32_e32 v6, v92, v136
	v_mul_f32_e32 v6, 0x3fb8aa3b, v6
	v_exp_f32_e32 v131, v6
	v_sub_f32_e32 v6, v96, v136
	v_mul_f32_e32 v6, 0x3fb8aa3b, v6
	v_exp_f32_e32 v92, v6
	v_sub_f32_e32 v6, v91, v136
	v_mul_f32_e32 v6, 0x3fb8aa3b, v6
	v_exp_f32_e32 v96, v6
	v_sub_f32_e32 v6, v95, v136
	v_mul_f32_e32 v6, 0x3fb8aa3b, v6
	v_exp_f32_e32 v91, v6
	v_sub_f32_e32 v6, v94, v136
	v_mul_f32_e32 v6, 0x3fb8aa3b, v6
	v_exp_f32_e32 v95, v6
	v_sub_f32_e32 v6, v99, v136
	v_mul_f32_e32 v6, 0x3fb8aa3b, v6
	v_exp_f32_e32 v94, v6
	v_sub_f32_e32 v6, v93, v136
	v_mul_f32_e32 v6, 0x3fb8aa3b, v6
	v_exp_f32_e32 v99, v6
	v_sub_f32_e32 v6, v97, v136
	v_mul_f32_e32 v6, 0x3fb8aa3b, v6
	v_exp_f32_e32 v93, v6
	v_cvt_pk_bf16_f32 v162, v131, v96
	v_cvt_pk_bf16_f32 v163, v95, v99
	v_cvt_pk_bf16_f32 v164, v92, v91
	v_cvt_pk_bf16_f32 v165, v94, v93
	v_add_u32_e32 v7, 0x800, v8
	v_add_u32_e32 v6, 0x1000, v8
	s_waitcnt lgkmcnt(0)
	v_mfma_f32_16x16x32_bf16 v[182:185], v[158:161], v[162:165], 0
	v_lshl_add_u64 v[158:159], v[86:87], 0, v[70:71]
	ds_read2_b64 v[166:169], v7 offset0:32 offset1:36
	ds_read2_b64 v[178:181], v6 offset0:64 offset1:68
	v_lshl_add_u64 v[86:87], v[86:87], 0, v[80:81]
	v_lshl_add_u64 v[248:249], v[158:159], 0, 0
	v_lshl_add_u64 v[238:239], v[86:87], 0, 0
	global_load_dwordx4 v[186:189], v[158:159], off
	global_load_dwordx4 v[190:193], v[86:87], off
	global_load_dword v250, v[248:249], off offset:128
	global_load_dword v251, v[238:239], off offset:128
	v_sub_f32_e32 v9, v100, v136
	v_mul_f32_e32 v9, 0x3fb8aa3b, v9
	v_add_u32_e32 v158, 0x1800, v8
	v_exp_f32_e32 v86, v9
	v_sub_f32_e32 v9, v105, v136
	ds_read2_b64 v[194:197], v158 offset0:96 offset1:100
	v_mul_f32_e32 v9, 0x3fb8aa3b, v9
	v_exp_f32_e32 v76, v9
	v_sub_f32_e32 v9, v98, v136
	v_mul_f32_e32 v9, 0x3fb8aa3b, v9
	v_exp_f32_e32 v90, v9
	v_sub_f32_e32 v9, v103, v136
	v_mul_f32_e32 v9, 0x3fb8aa3b, v9
	v_exp_f32_e32 v87, v9
	v_sub_f32_e32 v9, v102, v136
	v_mul_f32_e32 v9, 0x3fb8aa3b, v9
	v_exp_f32_e32 v98, v9
	v_sub_f32_e32 v9, v109, v136
	v_mul_f32_e32 v9, 0x3fb8aa3b, v9
	v_add_u32_e32 v160, 0x4800, v8
	s_waitcnt lgkmcnt(2)
	v_mfma_f32_16x16x32_bf16 v[166:169], v[166:169], v[162:165], 0
	s_waitcnt vmcnt(7)
	ds_write_b128 v75, v[170:173] offset:18432
	s_waitcnt vmcnt(6)
	ds_write_b128 v75, v[174:177] offset:27648
	s_waitcnt lgkmcnt(0)
	s_barrier
; #define LAS __attribute__((address_space(3)))
; __device__ __forceinline__ unsigned cvt_pk_bf16(float lo, float hi) { const float __attribute__((ext_vector_type(2))) v = {lo, hi}; return __builtin_bit_cast(unsigned, __builtin_convertvector(v, bf16x2_t)); }
; template <bool LOCAL>
; __device__ __forceinline__ void na_unit(const bf16* P, const bf16* VT, bf16* YCAT, const LAS float* rpb_l, LAS bf16* buf, int b, int gr, int hp, int qblk, int tid) {
;     ...
;             const int c = sidx - NCH;
;             if (LOCAL && c < 8) {
;                 float p[8];
; #pragma unroll
;                 for (int e = 0; e < 4; ++e) { p[e] = __expf(sl[2 * (c < 8 ? c : 0)][e] - m); p[4 + e] = __expf(sl[2 * (c < 8 ? c : 0) + 1][e] - m); }
; #pragma unroll
;                 for (int e = 0; e < 8; ++e) lsum += p[e];
;                 const bf16x8 pf = __builtin_bit_cast(bf16x8, (v4u){pg8::cvt_pk_bf16(p[0], p[1]), pg8::cvt_pk_bf16(p[2], p[3]), pg8::cvt_pk_bf16(p[4], p[5]), pg8::cvt_pk_bf16(p[6], p[7])});
; #pragma unroll
;                 for (int dt = 0; dt < 4; ++dt) { const LAS bf16* vp = cb + (16 * dt + fr) * 72 + kc0 + 4 * fq;
;                     o[dt] = __builtin_amdgcn_mfma_f32_16x16x32_bf16(frag44(vp, vp + 16), pf, o[dt], 0, 0, 0); }
;             } else {
;                 const int cc = c - NLOC;
; #pragma unroll
;                 for (int p2 = 0; p2 < 2; ++p2) {
;                     float p[8];
; #pragma unroll
;                     for (int e = 0; e < 4; ++e) { p[e] = __expf(sc[4 * (cc >= 0 ? cc : 0) + 2 * p2][e] - m); p[4 + e] = __expf(sc[4 * (cc >= 0 ? cc : 0) + 2 * p2 + 1][e] - m); }
; #pragma unroll
;                     for (int e = 0; e < 8; ++e) lsum += p[e];
;                     const bf16x8 pf = __builtin_bit_cast(bf16x8, (v4u){pg8::cvt_pk_bf16(p[0], p[1]), pg8::cvt_pk_bf16(p[2], p[3]), pg8::cvt_pk_bf16(p[4], p[5]), pg8::cvt_pk_bf16(p[6], p[7])});
; #pragma unroll
;                     for (int dt = 0; dt < 4; ++dt) { const LAS bf16* vp = cb + (16 * dt + fr) * 72 + 32 * p2 + 4 * fq;
;                         o[dt] = __builtin_amdgcn_mfma_f32_16x16x32_bf16(frag44(vp, vp + 16), pf, o[dt], 0, 0, 0); }
;                 }
;             }
;         }
;         if (sidx + 1 < 2 * NCH) NA_STORE(sidx + 1);
	v_mfma_f32_16x16x32_bf16 v[178:181], v[178:181], v[162:165], 0
	v_exp_f32_e32 v97, v9
	v_sub_f32_e32 v9, v101, v136
	v_mfma_f32_16x16x32_bf16 v[194:197], v[194:197], v[162:165], 0
	ds_read2_b64 v[162:165], v160 offset1:4
	v_add_u32_e32 v159, 0x5000, v8
	v_mul_f32_e32 v9, 0x3fb8aa3b, v9
	ds_read2_b64 v[170:173], v159 offset0:32 offset1:36
	v_exp_f32_e32 v100, v9
	v_sub_f32_e32 v9, v107, v136
	v_mul_f32_e32 v9, 0x3fb8aa3b, v9
	v_exp_f32_e32 v101, v9
	v_cvt_pk_bf16_f32 v174, v86, v90
	v_cvt_pk_bf16_f32 v175, v98, v100
	v_cvt_pk_bf16_f32 v176, v76, v87
	v_cvt_pk_bf16_f32 v177, v97, v101
	v_lshl_add_u64 v[102:103], s[0:1], 1, v[78:79]
	v_add_u32_e32 v161, 0x5800, v8
	s_waitcnt lgkmcnt(1)
	v_mfma_f32_16x16x32_bf16 v[182:185], v[162:165], v[174:177], v[182:185]
	v_lshl_add_u64 v[162:163], v[102:103], 0, v[70:71]
	v_lshl_add_u64 v[102:103], v[102:103], 0, v[80:81]
	v_sub_f32_e32 v9, v106, v136
	s_waitcnt lgkmcnt(0)
	v_mfma_f32_16x16x32_bf16 v[164:167], v[170:173], v[174:177], v[166:169]
	v_mul_f32_e32 v9, 0x3fb8aa3b, v9
	v_fma_f32 v62, v62, s71, -v136
	v_fma_f32 v63, v63, s71, -v136
	ds_read2_b64 v[168:171], v161 offset0:64 offset1:68
	v_lshl_add_u64 v[248:249], v[162:163], 0, 0
	v_lshl_add_u64 v[238:239], v[102:103], 0, 0
	global_load_dwordx4 v[198:201], v[162:163], off
	global_load_dwordx4 v[202:205], v[102:103], off
	global_load_dword v250, v[248:249], off offset:128
	global_load_dword v251, v[238:239], off offset:128
	v_add_u32_e32 v162, 0x6000, v8
	v_exp_f32_e32 v103, v9
	v_sub_f32_e32 v9, v113, v136
	s_waitcnt lgkmcnt(0)
	v_mfma_f32_16x16x32_bf16 v[168:171], v[168:171], v[174:177], v[178:181]
	s_nop 2
	ds_read2_b64 v[178:181], v162 offset0:96 offset1:100
	v_mul_f32_e32 v9, 0x3fb8aa3b, v9
	v_exp_f32_e32 v102, v9
	v_sub_f32_e32 v9, v104, v136
	v_mul_f32_e32 v9, 0x3fb8aa3b, v9
	v_exp_f32_e32 v105, v9
	v_sub_f32_e32 v9, v111, v136
	v_mul_f32_e32 v9, 0x3fb8aa3b, v9
	v_exp_f32_e32 v104, v9
	v_sub_f32_e32 v9, v110, v136
	v_mul_f32_e32 v9, 0x3fb8aa3b, v9
	v_exp_f32_e32 v107, v9
	v_sub_f32_e32 v9, v116, v136
	v_mul_f32_e32 v9, 0x3fb8aa3b, v9
	s_waitcnt lgkmcnt(0)
	v_mfma_f32_16x16x32_bf16 v[172:175], v[178:181], v[174:177], v[194:197]
	s_waitcnt vmcnt(7)
	ds_write_b128 v75, v[186:189]
	s_waitcnt vmcnt(6)
	ds_write_b128 v75, v[190:193] offset:9216
	s_waitcnt lgkmcnt(0)
	s_barrier
	v_exp_f32_e32 v106, v9
	v_sub_f32_e32 v9, v108, v136
	ds_read2_b64 v[176:179], v8 offset1:4
	v_mul_f32_e32 v9, 0x3fb8aa3b, v9
	v_exp_f32_e32 v108, v9
	v_sub_f32_e32 v9, v112, v136
	v_mul_f32_e32 v9, 0x3fb8aa3b, v9
	v_exp_f32_e32 v109, v9
	v_lshl_add_u64 v[190:191], s[18:19], 1, v[78:79]
	v_cvt_pk_bf16_f32 v186, v103, v105
	v_cvt_pk_bf16_f32 v187, v107, v108
	v_cvt_pk_bf16_f32 v188, v102, v104
	v_cvt_pk_bf16_f32 v189, v106, v109
	v_lshl_add_u64 v[194:195], v[190:191], 0, v[80:81]
	ds_read2_b64 v[110:113], v7 offset0:32 offset1:36
	s_waitcnt lgkmcnt(1)
	v_mfma_f32_16x16x32_bf16 v[176:179], v[176:179], v[186:189], v[182:185]
	v_sub_f32_e32 v9, v115, v136
	v_mul_f32_e32 v9, 0x3fb8aa3b, v9
	v_fma_f32 v64, v64, s71, -v136
	v_lshl_add_u64 v[184:185], v[190:191], 0, v[70:71]
	ds_read2_b64 v[180:183], v6 offset0:64 offset1:68
	v_lshl_add_u64 v[248:249], v[184:185], 0, 0
	v_lshl_add_u64 v[238:239], v[194:195], 0, 0
	global_load_dwordx4 v[190:193], v[184:185], off
	s_nop 0
	global_load_dwordx4 v[194:197], v[194:195], off
	global_load_dword v250, v[248:249], off offset:128
	global_load_dword v251, v[238:239], off offset:128
	s_waitcnt lgkmcnt(1)
	v_mfma_f32_16x16x32_bf16 v[164:167], v[110:113], v[186:189], v[164:167]
	ds_read2_b64 v[110:113], v158 offset0:96 offset1:100
	s_waitcnt vmcnt(7)
	ds_write_b128 v75, v[198:201] offset:18432
	s_waitcnt vmcnt(6)
	ds_write_b128 v75, v[202:205] offset:27648
	s_waitcnt lgkmcnt(2)
	v_mfma_f32_16x16x32_bf16 v[172:175], v[110:113], v[186:189], v[172:175]
	v_exp_f32_e32 v111, v9
	v_sub_f32_e32 v9, v121, v136
	v_mul_f32_e32 v9, 0x3fb8aa3b, v9
	v_exp_f32_e32 v110, v9
	v_sub_f32_e32 v9, v114, v136
	v_mul_f32_e32 v9, 0x3fb8aa3b, v9
	v_exp_f32_e32 v113, v9
	v_sub_f32_e32 v9, v119, v136
	v_mul_f32_e32 v9, 0x3fb8aa3b, v9
	v_exp_f32_e32 v112, v9
	v_sub_f32_e32 v9, v118, v136
	v_mul_f32_e32 v9, 0x3fb8aa3b, v9
	v_exp_f32_e32 v115, v9
	v_sub_f32_e32 v9, v124, v136
	v_mul_f32_e32 v9, 0x3fb8aa3b, v9
	v_exp_f32_e32 v114, v9
	v_sub_f32_e32 v9, v117, v136
	v_mul_f32_e32 v9, 0x3fb8aa3b, v9
	v_mfma_f32_16x16x32_bf16 v[168:171], v[180:183], v[186:189], v[168:171]
	s_waitcnt lgkmcnt(0)
	s_barrier
	v_exp_f32_e32 v116, v9
	ds_read2_b64 v[180:183], v160 offset1:4
	v_sub_f32_e32 v9, v120, v136
	ds_read2_b64 v[118:121], v159 offset0:32 offset1:36
	v_mul_f32_e32 v9, 0x3fb8aa3b, v9
	v_exp_f32_e32 v117, v9
	v_lshl_add_u64 v[188:189], s[20:21], 1, v[78:79]
	v_lshl_add_u64 v[198:199], v[188:189], 0, v[70:71]
	v_cvt_pk_bf16_f32 v184, v111, v113
	v_cvt_pk_bf16_f32 v185, v115, v116
	v_cvt_pk_bf16_f32 v186, v110, v112
	v_cvt_pk_bf16_f32 v187, v114, v117
	v_lshl_add_u64 v[188:189], v[188:189], 0, v[80:81]
	v_sub_f32_e32 v9, v123, v136
	s_waitcnt lgkmcnt(1)
	v_mfma_f32_16x16x32_bf16 v[176:179], v[180:183], v[184:187], v[176:179]
	v_lshl_add_u64 v[248:249], v[198:199], 0, 0
	v_lshl_add_u64 v[238:239], v[188:189], 0, 0
	global_load_dwordx4 v[180:183], v[198:199], off
	s_nop 0
	global_load_dwordx4 v[198:201], v[188:189], off
	global_load_dword v250, v[248:249], off offset:128
	global_load_dword v251, v[238:239], off offset:128
	v_mul_f32_e32 v9, 0x3fb8aa3b, v9
	v_fma_f32 v65, v65, s71, -v136
	s_waitcnt lgkmcnt(0)
	v_mfma_f32_16x16x32_bf16 v[164:167], v[118:121], v[184:187], v[164:167]
	ds_read2_b64 v[118:121], v161 offset0:64 offset1:68
	v_mul_f32_e32 v62, 0x3fb8aa3b, v62
	v_mul_f32_e32 v63, 0x3fb8aa3b, v63
	s_waitcnt lgkmcnt(0)
	v_mfma_f32_16x16x32_bf16 v[168:171], v[118:121], v[184:187], v[168:171]
	ds_read2_b64 v[118:121], v162 offset0:96 offset1:100
	s_waitcnt vmcnt(7)
	ds_write_b128 v75, v[190:193]
	s_waitcnt vmcnt(6)
	ds_write_b128 v75, v[194:197] offset:9216
	s_waitcnt lgkmcnt(0)
	v_mfma_f32_16x16x32_bf16 v[172:175], v[118:121], v[184:187], v[172:175]
	v_exp_f32_e32 v119, v9
	v_sub_f32_e32 v9, v129, v136
	v_mul_f32_e32 v9, 0x3fb8aa3b, v9
	v_exp_f32_e32 v118, v9
	v_sub_f32_e32 v9, v122, v136
	v_mul_f32_e32 v9, 0x3fb8aa3b, v9
	v_exp_f32_e32 v121, v9
	v_sub_f32_e32 v9, v127, v136
	v_mul_f32_e32 v9, 0x3fb8aa3b, v9
	v_exp_f32_e32 v120, v9
	v_sub_f32_e32 v9, v126, v136
	v_mul_f32_e32 v9, 0x3fb8aa3b, v9
	v_exp_f32_e32 v123, v9
	v_sub_f32_e32 v9, v133, v136
	v_mul_f32_e32 v9, 0x3fb8aa3b, v9
	s_barrier
; #define LAS __attribute__((address_space(3)))
; __device__ __forceinline__ unsigned cvt_pk_bf16(float lo, float hi) { const float __attribute__((ext_vector_type(2))) v = {lo, hi}; return __builtin_bit_cast(unsigned, __builtin_convertvector(v, bf16x2_t)); }
; template <bool LOCAL>
; __device__ __forceinline__ void na_unit(const bf16* P, const bf16* VT, bf16* YCAT, const LAS float* rpb_l, LAS bf16* buf, int b, int gr, int hp, int qblk, int tid) {
;     ...
;             const int c = sidx - NCH;
;             if (LOCAL && c < 8) {
;                 float p[8];
; #pragma unroll
;                 for (int e = 0; e < 4; ++e) { p[e] = __expf(sl[2 * (c < 8 ? c : 0)][e] - m); p[4 + e] = __expf(sl[2 * (c < 8 ? c : 0) + 1][e] - m); }
; #pragma unroll
;                 for (int e = 0; e < 8; ++e) lsum += p[e];
;                 const bf16x8 pf = __builtin_bit_cast(bf16x8, (v4u){pg8::cvt_pk_bf16(p[0], p[1]), pg8::cvt_pk_bf16(p[2], p[3]), pg8::cvt_pk_bf16(p[4], p[5]), pg8::cvt_pk_bf16(p[6], p[7])});
; #pragma unroll
;                 for (int dt = 0; dt < 4; ++dt) { const LAS bf16* vp = cb + (16 * dt + fr) * 72 + kc0 + 4 * fq;
;                     o[dt] = __builtin_amdgcn_mfma_f32_16x16x32_bf16(frag44(vp, vp + 16), pf, o[dt], 0, 0, 0); }
;             } else {
;                 const int cc = c - NLOC;
; #pragma unroll
;                 for (int p2 = 0; p2 < 2; ++p2) {
;                     float p[8];
; #pragma unroll
;                     for (int e = 0; e < 4; ++e) { p[e] = __expf(sc[4 * (cc >= 0 ? cc : 0) + 2 * p2][e] - m); p[4 + e] = __expf(sc[4 * (cc >= 0 ? cc : 0) + 2 * p2 + 1][e] - m); }
; #pragma unroll
;                     for (int e = 0; e < 8; ++e) lsum += p[e];
;                     const bf16x8 pf = __builtin_bit_cast(bf16x8, (v4u){pg8::cvt_pk_bf16(p[0], p[1]), pg8::cvt_pk_bf16(p[2], p[3]), pg8::cvt_pk_bf16(p[4], p[5]), pg8::cvt_pk_bf16(p[6], p[7])});
; #pragma unroll
;                     for (int dt = 0; dt < 4; ++dt) { const LAS bf16* vp = cb + (16 * dt + fr) * 72 + 32 * p2 + 4 * fq;
;                         o[dt] = __builtin_amdgcn_mfma_f32_16x16x32_bf16(frag44(vp, vp + 16), pf, o[dt], 0, 0, 0); }
;                 }
;             }
;         }
;         if (sidx + 1 < 2 * NCH) NA_STORE(sidx + 1);
	v_exp_f32_e32 v122, v9
	v_sub_f32_e32 v9, v125, v136
	ds_read2_b64 v[184:187], v8 offset1:4
	v_mul_f32_e32 v9, 0x3fb8aa3b, v9
	v_exp_f32_e32 v124, v9
	v_sub_f32_e32 v9, v128, v136
	v_mul_f32_e32 v9, 0x3fb8aa3b, v9
	v_exp_f32_e32 v125, v9
	v_lshl_add_u64 v[192:193], s[22:23], 1, v[78:79]
	v_cvt_pk_bf16_f32 v188, v119, v121
	v_cvt_pk_bf16_f32 v189, v123, v124
	v_cvt_pk_bf16_f32 v190, v118, v120
	v_cvt_pk_bf16_f32 v191, v122, v125
	v_lshl_add_u64 v[194:195], v[192:193], 0, v[70:71]
	ds_read2_b64 v[126:129], v7 offset0:32 offset1:36
	s_waitcnt lgkmcnt(1)
	v_mfma_f32_16x16x32_bf16 v[176:179], v[184:187], v[188:191], v[176:179]
	ds_read2_b64 v[184:187], v6 offset0:64 offset1:68
	v_lshl_add_u64 v[196:197], v[192:193], 0, v[80:81]
	v_lshl_add_u64 v[248:249], v[194:195], 0, 0
	v_lshl_add_u64 v[238:239], v[196:197], 0, 0
	global_load_dwordx4 v[192:195], v[194:195], off
	s_nop 0
	global_load_dwordx4 v[202:205], v[196:197], off
	global_load_dword v250, v[248:249], off offset:128
	global_load_dword v251, v[238:239], off offset:128
	s_waitcnt lgkmcnt(1)
	v_mfma_f32_16x16x32_bf16 v[164:167], v[126:129], v[188:191], v[164:167]
	ds_read2_b64 v[126:129], v158 offset0:96 offset1:100
	v_sub_f32_e32 v9, v132, v136
	v_mul_f32_e32 v9, 0x3fb8aa3b, v9
	s_waitcnt lgkmcnt(0)
	v_mfma_f32_16x16x32_bf16 v[172:175], v[126:129], v[188:191], v[172:175]
	v_exp_f32_e32 v127, v9
	v_sub_f32_e32 v9, v139, v136
	v_mul_f32_e32 v9, 0x3fb8aa3b, v9
	v_exp_f32_e32 v126, v9
	v_sub_f32_e32 v9, v130, v136
	v_mul_f32_e32 v9, 0x3fb8aa3b, v9
	v_exp_f32_e32 v129, v9
	v_sub_f32_e32 v9, v137, v136
	v_mul_f32_e32 v9, 0x3fb8aa3b, v9
	v_exp_f32_e32 v128, v9
	v_sub_f32_e32 v9, v135, v136
	v_mul_f32_e32 v9, 0x3fb8aa3b, v9
	v_exp_f32_e32 v132, v9
	v_sub_f32_e32 v9, v142, v136
	v_mul_f32_e32 v9, 0x3fb8aa3b, v9
	v_mfma_f32_16x16x32_bf16 v[168:171], v[184:187], v[188:191], v[168:171]
	s_waitcnt vmcnt(7)
	ds_write_b128 v75, v[180:183] offset:18432
	s_waitcnt vmcnt(6)
	ds_write_b128 v75, v[198:201] offset:27648
	s_waitcnt lgkmcnt(0)
	s_barrier
	v_exp_f32_e32 v130, v9
	v_sub_f32_e32 v9, v134, v136
	ds_read2_b64 v[180:183], v160 offset1:4
	ds_read2_b64 v[184:187], v159 offset0:32 offset1:36
	v_mul_f32_e32 v9, 0x3fb8aa3b, v9
	v_exp_f32_e32 v133, v9
	v_sub_f32_e32 v9, v138, v136
	v_mul_f32_e32 v9, 0x3fb8aa3b, v9
	v_exp_f32_e32 v134, v9
	v_lshl_add_u64 v[196:197], s[24:25], 1, v[78:79]
	v_lshl_add_u64 v[198:199], v[196:197], 0, v[70:71]
	v_cvt_pk_bf16_f32 v188, v127, v129
	v_cvt_pk_bf16_f32 v189, v132, v133
	v_cvt_pk_bf16_f32 v190, v126, v128
	v_cvt_pk_bf16_f32 v191, v130, v134
	v_lshl_add_u64 v[138:139], v[196:197], 0, v[80:81]
	v_sub_f32_e32 v9, v141, v136
	s_waitcnt lgkmcnt(1)
	v_mfma_f32_16x16x32_bf16 v[176:179], v[180:183], v[188:191], v[176:179]
	global_load_dwordx4 v[180:183], v[198:199], off
	s_nop 0
	global_load_dwordx4 v[196:199], v[138:139], off
	v_mul_f32_e32 v9, 0x3fb8aa3b, v9
	v_exp_f32_e32 v137, v9
	s_waitcnt lgkmcnt(0)
	v_mfma_f32_16x16x32_bf16 v[164:167], v[184:187], v[188:191], v[164:167]
	ds_read2_b64 v[184:187], v161 offset0:64 offset1:68
	v_sub_f32_e32 v9, v147, v136
	v_mul_f32_e32 v9, 0x3fb8aa3b, v9
	s_waitcnt lgkmcnt(0)
	v_mfma_f32_16x16x32_bf16 v[168:171], v[184:187], v[188:191], v[168:171]
	ds_read2_b64 v[184:187], v162 offset0:96 offset1:100
	v_exp_f32_e32 v135, v9
	v_sub_f32_e32 v9, v140, v136
	v_mul_f32_e32 v9, 0x3fb8aa3b, v9
	v_exp_f32_e32 v139, v9
	v_sub_f32_e32 v9, v145, v136
	v_mul_f32_e32 v9, 0x3fb8aa3b, v9
	v_exp_f32_e32 v138, v9
	v_sub_f32_e32 v9, v144, v136
	v_mul_f32_e32 v9, 0x3fb8aa3b, v9
	s_waitcnt lgkmcnt(0)
	v_mfma_f32_16x16x32_bf16 v[172:175], v[184:187], v[188:191], v[172:175]
	s_waitcnt vmcnt(5)
	ds_write_b128 v75, v[192:195]
	s_waitcnt vmcnt(4)
	ds_write_b128 v75, v[202:205] offset:9216
	s_waitcnt lgkmcnt(0)
	s_barrier
	v_exp_f32_e32 v141, v9
	v_sub_f32_e32 v9, v150, v136
	ds_read2_b64 v[184:187], v8 offset1:4
	v_mul_f32_e32 v9, 0x3fb8aa3b, v9
	ds_read2_b64 v[188:191], v7 offset0:32 offset1:36
	v_exp_f32_e32 v140, v9
	v_sub_f32_e32 v9, v143, v136
	v_sub_f32_e32 v8, v146, v136
	v_mul_f32_e32 v9, 0x3fb8aa3b, v9
	v_mul_f32_e32 v8, 0x3fb8aa3b, v8
	v_exp_f32_e32 v142, v9
	v_exp_f32_e32 v143, v8
	v_cvt_pk_bf16_f32 v144, v137, v139
	v_cvt_pk_bf16_f32 v146, v135, v138
	v_cvt_pk_bf16_f32 v145, v141, v142
	v_cvt_pk_bf16_f32 v147, v140, v143
	v_lshl_add_u64 v[8:9], s[26:27], 1, v[78:79]
	v_mul_f32_e32 v64, 0x3fb8aa3b, v64
	s_waitcnt lgkmcnt(1)
	v_mfma_f32_16x16x32_bf16 v[176:179], v[184:187], v[144:147], v[176:179]
	ds_read2_b64 v[184:187], v6 offset0:64 offset1:68
	v_lshl_add_u64 v[6:7], v[8:9], 0, v[70:71]
	v_lshl_add_u64 v[8:9], v[8:9], 0, v[80:81]
	s_waitcnt lgkmcnt(1)
	v_mfma_f32_16x16x32_bf16 v[164:167], v[188:191], v[144:147], v[164:167]
	v_lshl_add_u64 v[248:249], v[6:7], 0, 0
	v_lshl_add_u64 v[238:239], v[8:9], 0, 0
	global_load_dwordx4 v[188:191], v[6:7], off
	global_load_dwordx4 v[192:195], v[8:9], off
	global_load_dword v250, v[248:249], off offset:128
	global_load_dword v251, v[238:239], off offset:128
	ds_read2_b64 v[78:81], v158 offset0:96 offset1:100
	s_waitcnt vmcnt(5)
	ds_write_b128 v75, v[180:183] offset:18432
	s_waitcnt vmcnt(4)
	ds_write_b128 v75, v[196:199] offset:27648
	s_waitcnt lgkmcnt(3)
	v_mfma_f32_16x16x32_bf16 v[168:171], v[184:187], v[144:147], v[168:171]
	s_waitcnt lgkmcnt(0)
	s_barrier
; #define LAS __attribute__((address_space(3)))
; __device__ __forceinline__ unsigned cvt_pk_bf16(float lo, float hi) { const float __attribute__((ext_vector_type(2))) v = {lo, hi}; return __builtin_bit_cast(unsigned, __builtin_convertvector(v, bf16x2_t)); }
; template <bool LOCAL>
; __device__ __forceinline__ void na_unit(const bf16* P, const bf16* VT, bf16* YCAT, const LAS float* rpb_l, LAS bf16* buf, int b, int gr, int hp, int qblk, int tid) {
;     ...
;             const int c = sidx - NCH;
;             if (LOCAL && c < 8) {
;                 float p[8];
; #pragma unroll
;                 for (int e = 0; e < 4; ++e) { p[e] = __expf(sl[2 * (c < 8 ? c : 0)][e] - m); p[4 + e] = __expf(sl[2 * (c < 8 ? c : 0) + 1][e] - m); }
; #pragma unroll
;                 for (int e = 0; e < 8; ++e) lsum += p[e];
;                 const bf16x8 pf = __builtin_bit_cast(bf16x8, (v4u){pg8::cvt_pk_bf16(p[0], p[1]), pg8::cvt_pk_bf16(p[2], p[3]), pg8::cvt_pk_bf16(p[4], p[5]), pg8::cvt_pk_bf16(p[6], p[7])});
; #pragma unroll
;                 for (int dt = 0; dt < 4; ++dt) { const LAS bf16* vp = cb + (16 * dt + fr) * 72 + kc0 + 4 * fq;
;                     o[dt] = __builtin_amdgcn_mfma_f32_16x16x32_bf16(frag44(vp, vp + 16), pf, o[dt], 0, 0, 0); }
;             } else {
;                 const int cc = c - NLOC;
; #pragma unroll
;                 for (int p2 = 0; p2 < 2; ++p2) {
;                     float p[8];
; #pragma unroll
;                     for (int e = 0; e < 4; ++e) { p[e] = __expf(sc[4 * (cc >= 0 ? cc : 0) + 2 * p2][e] - m); p[4 + e] = __expf(sc[4 * (cc >= 0 ? cc : 0) + 2 * p2 + 1][e] - m); }
; #pragma unroll
;                     for (int e = 0; e < 8; ++e) lsum += p[e];
;                     const bf16x8 pf = __builtin_bit_cast(bf16x8, (v4u){pg8::cvt_pk_bf16(p[0], p[1]), pg8::cvt_pk_bf16(p[2], p[3]), pg8::cvt_pk_bf16(p[4], p[5]), pg8::cvt_pk_bf16(p[6], p[7])});
; #pragma unroll
;                     for (int dt = 0; dt < 4; ++dt) { const LAS bf16* vp = cb + (16 * dt + fr) * 72 + 32 * p2 + 4 * fq;
;                         o[dt] = __builtin_amdgcn_mfma_f32_16x16x32_bf16(frag44(vp, vp + 16), pf, o[dt], 0, 0, 0); }
;                 }
;             }
;         }
;         if (sidx + 1 < 2 * NCH) NA_STORE(sidx + 1);
	v_mfma_f32_16x16x32_bf16 v[172:175], v[78:81], v[144:147], v[172:175]
	v_sub_f32_e32 v70, v149, v136
	v_sub_f32_e32 v79, v148, v136
	v_sub_f32_e32 v81, v152, v136
	v_sub_f32_e32 v145, v151, v136
	ds_read2_b64 v[148:151], v160 offset1:4
	v_mul_f32_e32 v70, 0x3fb8aa3b, v70
	v_mul_f32_e32 v79, 0x3fb8aa3b, v79
	v_mul_f32_e32 v81, 0x3fb8aa3b, v81
	v_mul_f32_e32 v145, 0x3fb8aa3b, v145
	v_exp_f32_e32 v78, v70
	v_sub_f32_e32 v70, v155, v136
	v_exp_f32_e32 v80, v79
	v_sub_f32_e32 v79, v153, v136
	v_exp_f32_e32 v144, v81
	v_sub_f32_e32 v81, v157, v136
	v_exp_f32_e32 v146, v145
	v_sub_f32_e32 v145, v154, v136
	v_mul_f32_e32 v70, 0x3fb8aa3b, v70
	v_mul_f32_e32 v79, 0x3fb8aa3b, v79
	v_mul_f32_e32 v81, 0x3fb8aa3b, v81
	v_mul_f32_e32 v145, 0x3fb8aa3b, v145
	v_exp_f32_e32 v70, v70
	v_exp_f32_e32 v79, v79
	v_exp_f32_e32 v81, v81
	v_exp_f32_e32 v145, v145
	v_cvt_pk_bf16_f32 v152, v78, v80
	v_cvt_pk_bf16_f32 v153, v144, v146
	v_cvt_pk_bf16_f32 v154, v70, v79
	v_cvt_pk_bf16_f32 v155, v81, v145
	v_mul_f32_e32 v65, 0x3fb8aa3b, v65
	v_exp_f32_e32 v147, v62
	s_waitcnt lgkmcnt(0)
	v_mfma_f32_16x16x32_bf16 v[148:151], v[148:151], v[152:155], v[176:179]
	v_fma_f32 v62, v66, s71, -v136
	v_exp_f32_e32 v66, v63
	v_fma_f32 v63, v67, s71, -v136
	ds_read2_b64 v[176:179], v159 offset0:32 offset1:36
	ds_read2_b64 v[158:161], v161 offset0:64 offset1:68
	s_waitcnt lgkmcnt(0)
	v_mfma_f32_16x16x32_bf16 v[158:161], v[158:161], v[152:155], v[168:171]
	s_nop 2
	ds_read2_b64 v[168:171], v162 offset0:96 offset1:100
	v_exp_f32_e32 v67, v64
	v_fma_f32 v64, v68, s71, -v136
	v_mfma_f32_16x16x32_bf16 v[164:167], v[176:179], v[152:155], v[164:167]
	v_lshl_add_u64 v[248:249], v[6:7], 0, 0
	v_lshl_add_u64 v[238:239], v[8:9], 0, 0
	global_load_dwordx4 v[176:179], v[6:7], off offset:128
	global_load_dwordx4 v[180:183], v[8:9], off offset:128
	global_load_dword v250, v[248:249], off offset:256
	global_load_dword v251, v[238:239], off offset:256
	s_waitcnt vmcnt(7)
	ds_write_b128 v75, v[188:191]
	s_waitcnt vmcnt(6)
	ds_write_b128 v75, v[192:195] offset:9216
	s_waitcnt lgkmcnt(0)
	v_mfma_f32_16x16x32_bf16 v[152:155], v[168:171], v[152:155], v[172:175]
	s_barrier
	ds_read2_b64 v[168:171], v156 offset1:4
	v_exp_f32_e32 v68, v65
	v_fma_f32 v65, v69, s71, -v136
	v_mul_f32_e32 v62, 0x3fb8aa3b, v62
	v_mul_f32_e32 v63, 0x3fb8aa3b, v63
	v_mul_f32_e32 v64, 0x3fb8aa3b, v64
	v_mul_f32_e32 v65, 0x3fb8aa3b, v65
	v_exp_f32_e32 v62, v62
	v_exp_f32_e32 v63, v63
	v_exp_f32_e32 v64, v64
	v_exp_f32_e32 v65, v65
	v_cvt_pk_bf16_f32 v172, v147, v66
	v_cvt_pk_bf16_f32 v173, v67, v68
	v_cvt_pk_bf16_f32 v174, v62, v63
	v_cvt_pk_bf16_f32 v175, v64, v65
	v_add_u32_e32 v157, 0x800, v156
	v_add_u32_e32 v192, 0x1000, v156
	s_waitcnt lgkmcnt(0)
	v_mfma_f32_16x16x32_bf16 v[148:151], v[168:171], v[172:175], v[148:151]
	ds_read2_b64 v[168:171], v157 offset0:32 offset1:36
	v_add_u32_e32 v193, 0x1800, v156
	v_fma_f32 v58, v58, s71, -v136
	s_waitcnt lgkmcnt(0)
	v_mfma_f32_16x16x32_bf16 v[162:165], v[168:171], v[172:175], v[164:167]
	s_nop 2
	ds_read2_b64 v[166:169], v192 offset0:64 offset1:68
	v_fma_f32 v54, v54, s71, -v136
	v_fma_f32 v59, v59, s71, -v136
	s_waitcnt lgkmcnt(0)
	v_mfma_f32_16x16x32_bf16 v[158:161], v[166:169], v[172:175], v[158:161]
	ds_read2_b64 v[166:169], v193 offset0:96 offset1:100
	v_fma_f32 v55, v55, s71, -v136
	v_fma_f32 v60, v60, s71, -v136
	s_waitcnt lgkmcnt(0)
	v_mfma_f32_16x16x32_bf16 v[152:155], v[166:169], v[172:175], v[152:155]
	ds_read2_b64 v[166:169], v156 offset0:8 offset1:12
	v_fma_f32 v56, v56, s71, -v136
	v_fma_f32 v61, v61, s71, -v136
	v_fma_f32 v57, v57, s71, -v136
	v_mul_f32_e32 v58, 0x3fb8aa3b, v58
	v_mul_f32_e32 v54, 0x3fb8aa3b, v54
	v_mul_f32_e32 v59, 0x3fb8aa3b, v59
	v_mul_f32_e32 v55, 0x3fb8aa3b, v55
	v_mul_f32_e32 v60, 0x3fb8aa3b, v60
	v_mul_f32_e32 v56, 0x3fb8aa3b, v56
	v_mul_f32_e32 v61, 0x3fb8aa3b, v61
	v_mul_f32_e32 v57, 0x3fb8aa3b, v57
	v_exp_f32_e32 v58, v58
	v_exp_f32_e32 v54, v54
	v_exp_f32_e32 v59, v59
	v_exp_f32_e32 v55, v55
	v_exp_f32_e32 v60, v60
	v_exp_f32_e32 v56, v56
	v_exp_f32_e32 v61, v61
	v_exp_f32_e32 v57, v57
	v_cvt_pk_bf16_f32 v170, v58, v59
	v_cvt_pk_bf16_f32 v172, v54, v55
	v_cvt_pk_bf16_f32 v171, v60, v61
	v_cvt_pk_bf16_f32 v173, v56, v57
	v_fma_f32 v46, v46, s71, -v136
	v_fma_f32 v47, v47, s71, -v136
	s_waitcnt lgkmcnt(0)
	v_mfma_f32_16x16x32_bf16 v[148:151], v[166:169], v[170:173], v[148:151]
	ds_read2_b64 v[166:169], v157 offset0:40 offset1:44
	v_fma_f32 v48, v48, s71, -v136
	v_mul_f32_e32 v46, 0x3fb8aa3b, v46
	s_waitcnt lgkmcnt(0)
	v_mfma_f32_16x16x32_bf16 v[162:165], v[166:169], v[170:173], v[162:165]
	ds_read2_b64 v[166:169], v192 offset0:72 offset1:76
	v_mul_f32_e32 v47, 0x3fb8aa3b, v47
	v_mul_f32_e32 v48, 0x3fb8aa3b, v48
	s_waitcnt lgkmcnt(0)
	v_mfma_f32_16x16x32_bf16 v[158:161], v[166:169], v[170:173], v[158:161]
	ds_read2_b64 v[166:169], v193 offset0:104 offset1:108
	v_exp_f32_e32 v69, v46
	v_fma_f32 v46, v50, s71, -v136
	v_exp_f32_e32 v50, v47
	v_fma_f32 v47, v51, s71, -v136
	v_exp_f32_e32 v51, v48
	v_fma_f32 v48, v52, s71, -v136
	v_add_u32_e32 v52, 0x4800, v156
	v_lshl_add_u64 v[248:249], v[6:7], 0, 0
	v_lshl_add_u64 v[238:239], v[8:9], 0, 0
	global_load_dwordx4 v[184:187], v[6:7], off offset:256
	global_load_dwordx4 v[188:191], v[8:9], off offset:256
	global_load_dword v250, v[248:249], off offset:384
	global_load_dword v251, v[238:239], off offset:384
	s_waitcnt lgkmcnt(0)
	v_mfma_f32_16x16x32_bf16 v[152:155], v[166:169], v[170:173], v[152:155]
	s_waitcnt vmcnt(7)
	ds_write_b128 v75, v[176:179] offset:18432
	s_waitcnt vmcnt(6)
	ds_write_b128 v75, v[180:183] offset:27648
	s_waitcnt lgkmcnt(0)
	s_barrier
; #define LAS __attribute__((address_space(3)))
; __device__ __forceinline__ unsigned cvt_pk_bf16(float lo, float hi) { const float __attribute__((ext_vector_type(2))) v = {lo, hi}; return __builtin_bit_cast(unsigned, __builtin_convertvector(v, bf16x2_t)); }
; template <bool LOCAL>
; __device__ __forceinline__ void na_unit(const bf16* P, const bf16* VT, bf16* YCAT, const LAS float* rpb_l, LAS bf16* buf, int b, int gr, int hp, int qblk, int tid) {
;     ...
;             const int c = sidx - NCH;
;             if (LOCAL && c < 8) {
;                 float p[8];
; #pragma unroll
;                 for (int e = 0; e < 4; ++e) { p[e] = __expf(sl[2 * (c < 8 ? c : 0)][e] - m); p[4 + e] = __expf(sl[2 * (c < 8 ? c : 0) + 1][e] - m); }
; #pragma unroll
;                 for (int e = 0; e < 8; ++e) lsum += p[e];
;                 const bf16x8 pf = __builtin_bit_cast(bf16x8, (v4u){pg8::cvt_pk_bf16(p[0], p[1]), pg8::cvt_pk_bf16(p[2], p[3]), pg8::cvt_pk_bf16(p[4], p[5]), pg8::cvt_pk_bf16(p[6], p[7])});
; #pragma unroll
;                 for (int dt = 0; dt < 4; ++dt) { const LAS bf16* vp = cb + (16 * dt + fr) * 72 + kc0 + 4 * fq;
;                     o[dt] = __builtin_amdgcn_mfma_f32_16x16x32_bf16(frag44(vp, vp + 16), pf, o[dt], 0, 0, 0); }
;             } else {
;                 const int cc = c - NLOC;
; #pragma unroll
;                 for (int p2 = 0; p2 < 2; ++p2) {
;                     float p[8];
; #pragma unroll
;                     for (int e = 0; e < 4; ++e) { p[e] = __expf(sc[4 * (cc >= 0 ? cc : 0) + 2 * p2][e] - m); p[4 + e] = __expf(sc[4 * (cc >= 0 ? cc : 0) + 2 * p2 + 1][e] - m); }
; #pragma unroll
;                     for (int e = 0; e < 8; ++e) lsum += p[e];
;                     const bf16x8 pf = __builtin_bit_cast(bf16x8, (v4u){pg8::cvt_pk_bf16(p[0], p[1]), pg8::cvt_pk_bf16(p[2], p[3]), pg8::cvt_pk_bf16(p[4], p[5]), pg8::cvt_pk_bf16(p[6], p[7])});
; #pragma unroll
;                     for (int dt = 0; dt < 4; ++dt) { const LAS bf16* vp = cb + (16 * dt + fr) * 72 + 32 * p2 + 4 * fq;
;                         o[dt] = __builtin_amdgcn_mfma_f32_16x16x32_bf16(frag44(vp, vp + 16), pf, o[dt], 0, 0, 0); }
;                 }
;             }
;         }
;         if (sidx + 1 < 2 * NCH) NA_STORE(sidx + 1);
	v_fma_f32 v49, v49, s71, -v136
	ds_read2_b64 v[166:169], v52 offset1:4
	v_mul_f32_e32 v49, 0x3fb8aa3b, v49
	v_exp_f32_e32 v174, v49
	v_fma_f32 v49, v53, s71, -v136
	v_mul_f32_e32 v46, 0x3fb8aa3b, v46
	v_mul_f32_e32 v47, 0x3fb8aa3b, v47
	v_mul_f32_e32 v48, 0x3fb8aa3b, v48
	v_mul_f32_e32 v49, 0x3fb8aa3b, v49
	v_exp_f32_e32 v46, v46
	v_exp_f32_e32 v47, v47
	v_exp_f32_e32 v48, v48
	v_exp_f32_e32 v53, v49
	v_cvt_pk_bf16_f32 v170, v69, v50
	v_cvt_pk_bf16_f32 v171, v51, v174
	v_cvt_pk_bf16_f32 v172, v46, v47
	v_cvt_pk_bf16_f32 v173, v48, v53
	v_add_u32_e32 v175, 0x5000, v156
	v_add_u32_e32 v176, 0x5800, v156
	s_waitcnt lgkmcnt(0)
	v_mfma_f32_16x16x32_bf16 v[148:151], v[166:169], v[170:173], v[148:151]
	ds_read2_b64 v[166:169], v175 offset0:32 offset1:36
	v_add_u32_e32 v49, 0x6000, v156
	v_fma_f32 v38, v38, s71, -v136
	s_waitcnt lgkmcnt(0)
	v_mfma_f32_16x16x32_bf16 v[162:165], v[166:169], v[170:173], v[162:165]
	ds_read2_b64 v[166:169], v176 offset0:64 offset1:68
	v_mul_f32_e32 v38, 0x3fb8aa3b, v38
	v_fma_f32 v42, v42, s71, -v136
	s_waitcnt lgkmcnt(0)
	v_mfma_f32_16x16x32_bf16 v[158:161], v[166:169], v[170:173], v[158:161]
	ds_read2_b64 v[166:169], v49 offset0:96 offset1:100
	v_mul_f32_e32 v42, 0x3fb8aa3b, v42
	v_fma_f32 v30, v30, s71, -v136
	s_waitcnt lgkmcnt(0)
	v_mfma_f32_16x16x32_bf16 v[152:155], v[166:169], v[170:173], v[152:155]
	v_exp_f32_e32 v171, v38
	v_fma_f32 v38, v43, s71, -v136
	v_mul_f32_e32 v38, 0x3fb8aa3b, v38
	v_exp_f32_e32 v172, v38
	v_fma_f32 v38, v39, s71, -v136
	v_mul_f32_e32 v38, 0x3fb8aa3b, v38
	v_exp_f32_e32 v173, v38
	v_fma_f32 v38, v44, s71, -v136
	v_mul_f32_e32 v38, 0x3fb8aa3b, v38
	v_exp_f32_e32 v177, v38
	v_fma_f32 v38, v40, s71, -v136
	v_mul_f32_e32 v38, 0x3fb8aa3b, v38
	v_exp_f32_e32 v170, v42
	v_exp_f32_e32 v178, v38
	v_fma_f32 v38, v45, s71, -v136
	ds_read2_b64 v[42:45], v52 offset0:8 offset1:12
	v_mul_f32_e32 v38, 0x3fb8aa3b, v38
	v_exp_f32_e32 v179, v38
	v_fma_f32 v38, v41, s71, -v136
	v_mul_f32_e32 v38, 0x3fb8aa3b, v38
	v_exp_f32_e32 v180, v38
	v_cvt_pk_bf16_f32 v38, v170, v172
	v_cvt_pk_bf16_f32 v39, v177, v179
	v_cvt_pk_bf16_f32 v40, v171, v173
	v_cvt_pk_bf16_f32 v41, v178, v180
	v_mul_f32_e32 v30, 0x3fb8aa3b, v30
	v_fma_f32 v22, v22, s71, -v136
	s_waitcnt lgkmcnt(0)
	v_mfma_f32_16x16x32_bf16 v[42:45], v[42:45], v[38:41], v[148:151]
	v_mul_f32_e32 v22, 0x3fb8aa3b, v22
	v_fma_f32 v26, v26, s71, -v136
	v_mul_f32_e32 v26, 0x3fb8aa3b, v26
	ds_read2_b64 v[148:151], v175 offset0:40 offset1:44
	s_waitcnt lgkmcnt(0)
	v_mfma_f32_16x16x32_bf16 v[148:151], v[148:151], v[38:41], v[162:165]
	s_nop 2
	ds_read2_b64 v[162:165], v176 offset0:72 offset1:76
	v_fma_f32 v2, v2, s71, -v136
	v_mul_f32_e32 v2, 0x3fb8aa3b, v2
	s_waitcnt lgkmcnt(0)
	v_mfma_f32_16x16x32_bf16 v[158:161], v[162:165], v[38:41], v[158:161]
	ds_read2_b64 v[162:165], v49 offset0:104 offset1:108
	global_load_dwordx4 v[166:169], v[6:7], off offset:384
	s_nop 0
	global_load_dwordx4 v[6:9], v[8:9], off offset:384
	s_waitcnt vmcnt(5)
	ds_write_b128 v75, v[184:187]
	s_waitcnt vmcnt(4)
	ds_write_b128 v75, v[188:191] offset:9216
	s_waitcnt lgkmcnt(2)
	v_mfma_f32_16x16x32_bf16 v[38:41], v[162:165], v[38:41], v[152:155]
	v_exp_f32_e32 v162, v30
	v_fma_f32 v30, v34, s71, -v136
	v_mul_f32_e32 v30, 0x3fb8aa3b, v30
	v_exp_f32_e32 v163, v30
	v_fma_f32 v30, v31, s71, -v136
	v_mul_f32_e32 v30, 0x3fb8aa3b, v30
	v_exp_f32_e32 v164, v30
	v_fma_f32 v30, v35, s71, -v136
	v_mul_f32_e32 v30, 0x3fb8aa3b, v30
	v_exp_f32_e32 v165, v30
	v_fma_f32 v30, v32, s71, -v136
	v_mul_f32_e32 v30, 0x3fb8aa3b, v30
	v_exp_f32_e32 v181, v30
	v_fma_f32 v30, v36, s71, -v136
	v_mul_f32_e32 v30, 0x3fb8aa3b, v30
	v_exp_f32_e32 v182, v30
	v_fma_f32 v30, v33, s71, -v136
	s_waitcnt lgkmcnt(0)
	s_barrier
	v_mul_f32_e32 v34, 0x3fb8aa3b, v30
	ds_read2_b64 v[30:33], v156 offset1:4
	v_exp_f32_e32 v183, v34
	v_fma_f32 v34, v37, s71, -v136
	v_mul_f32_e32 v34, 0x3fb8aa3b, v34
	v_exp_f32_e32 v184, v34
	v_cvt_pk_bf16_f32 v34, v162, v164
	v_cvt_pk_bf16_f32 v35, v181, v183
	v_cvt_pk_bf16_f32 v36, v163, v165
	v_cvt_pk_bf16_f32 v37, v182, v184
	ds_read2_b64 v[152:155], v193 offset0:96 offset1:100
	v_fma_f32 v10, v10, s71, -v136
	s_waitcnt lgkmcnt(1)
	v_mfma_f32_16x16x32_bf16 v[30:33], v[30:33], v[34:37], v[42:45]
	v_mul_f32_e32 v10, 0x3fb8aa3b, v10
	s_nop 1
	ds_read2_b64 v[42:45], v157 offset0:32 offset1:36
	s_waitcnt lgkmcnt(0)
	v_mfma_f32_16x16x32_bf16 v[42:45], v[42:45], v[34:37], v[148:151]
	s_nop 2
	ds_read2_b64 v[148:151], v192 offset0:64 offset1:68
	s_waitcnt lgkmcnt(0)
	v_mfma_f32_16x16x32_bf16 v[148:151], v[148:151], v[34:37], v[158:161]
	v_mfma_f32_16x16x32_bf16 v[34:37], v[152:155], v[34:37], v[38:41]
	v_exp_f32_e32 v153, v22
	v_fma_f32 v22, v27, s71, -v136
	v_mul_f32_e32 v22, 0x3fb8aa3b, v22
	v_exp_f32_e32 v154, v22
	v_fma_f32 v22, v23, s71, -v136
	v_mul_f32_e32 v22, 0x3fb8aa3b, v22
	v_exp_f32_e32 v155, v22
	v_fma_f32 v22, v28, s71, -v136
	v_mul_f32_e32 v22, 0x3fb8aa3b, v22
	v_exp_f32_e32 v158, v22
	v_fma_f32 v22, v24, s71, -v136
	v_mul_f32_e32 v22, 0x3fb8aa3b, v22
	v_exp_f32_e32 v152, v26
	v_exp_f32_e32 v159, v22
	v_fma_f32 v22, v29, s71, -v136
	ds_read2_b64 v[26:29], v156 offset0:8 offset1:12
	v_mul_f32_e32 v22, 0x3fb8aa3b, v22
	v_exp_f32_e32 v156, v22
	v_fma_f32 v22, v25, s71, -v136
	v_mul_f32_e32 v22, 0x3fb8aa3b, v22
	v_exp_f32_e32 v160, v22
	v_cvt_pk_bf16_f32 v22, v152, v154
	v_cvt_pk_bf16_f32 v23, v158, v156
	v_cvt_pk_bf16_f32 v24, v153, v155
	v_cvt_pk_bf16_f32 v25, v159, v160
	ds_read2_b64 v[38:41], v192 offset0:72 offset1:76
	s_waitcnt lgkmcnt(1)
	v_mfma_f32_16x16x32_bf16 v[26:29], v[26:29], v[22:25], v[30:33]
	s_nop 2
	ds_read2_b64 v[30:33], v157 offset0:40 offset1:44
	s_waitcnt lgkmcnt(0)
	v_mfma_f32_16x16x32_bf16 v[30:33], v[30:33], v[22:25], v[42:45]
	s_nop 2
	ds_read2_b64 v[42:45], v193 offset0:104 offset1:108
	s_waitcnt vmcnt(1)
	ds_write_b128 v75, v[166:169] offset:18432
	s_waitcnt vmcnt(0)
	ds_write_b128 v75, v[6:9] offset:27648
	v_fma_f32 v6, v14, s71, -v136
	v_mul_f32_e32 v6, 0x3fb8aa3b, v6
	v_mfma_f32_16x16x32_bf16 v[38:41], v[38:41], v[22:25], v[148:151]
	s_waitcnt lgkmcnt(0)
	s_barrier
; #define LAS __attribute__((address_space(3)))
; __device__ __forceinline__ unsigned cvt_pk_bf16(float lo, float hi) { const float __attribute__((ext_vector_type(2))) v = {lo, hi}; return __builtin_bit_cast(unsigned, __builtin_convertvector(v, bf16x2_t)); }
; template <bool LOCAL>
; __device__ __forceinline__ void na_unit(const bf16* P, const bf16* VT, bf16* YCAT, const LAS float* rpb_l, LAS bf16* buf, int b, int gr, int hp, int qblk, int tid) {
;     ...
;             const int c = sidx - NCH;
;             if (LOCAL && c < 8) {
;                 float p[8];
; #pragma unroll
;                 for (int e = 0; e < 4; ++e) { p[e] = __expf(sl[2 * (c < 8 ? c : 0)][e] - m); p[4 + e] = __expf(sl[2 * (c < 8 ? c : 0) + 1][e] - m); }
; #pragma unroll
;                 for (int e = 0; e < 8; ++e) lsum += p[e];
;                 const bf16x8 pf = __builtin_bit_cast(bf16x8, (v4u){pg8::cvt_pk_bf16(p[0], p[1]), pg8::cvt_pk_bf16(p[2], p[3]), pg8::cvt_pk_bf16(p[4], p[5]), pg8::cvt_pk_bf16(p[6], p[7])});
; #pragma unroll
;                 for (int dt = 0; dt < 4; ++dt) { const LAS bf16* vp = cb + (16 * dt + fr) * 72 + kc0 + 4 * fq;
;                     o[dt] = __builtin_amdgcn_mfma_f32_16x16x32_bf16(frag44(vp, vp + 16), pf, o[dt], 0, 0, 0); }
;             } else {
;                 const int cc = c - NLOC;
; #pragma unroll
;                 for (int p2 = 0; p2 < 2; ++p2) {
;                     float p[8];
; #pragma unroll
;                     for (int e = 0; e < 4; ++e) { p[e] = __expf(sc[4 * (cc >= 0 ? cc : 0) + 2 * p2][e] - m); p[4 + e] = __expf(sc[4 * (cc >= 0 ? cc : 0) + 2 * p2 + 1][e] - m); }
; #pragma unroll
;                     for (int e = 0; e < 8; ++e) lsum += p[e];
;                     const bf16x8 pf = __builtin_bit_cast(bf16x8, (v4u){pg8::cvt_pk_bf16(p[0], p[1]), pg8::cvt_pk_bf16(p[2], p[3]), pg8::cvt_pk_bf16(p[4], p[5]), pg8::cvt_pk_bf16(p[6], p[7])});
; #pragma unroll
;                     for (int dt = 0; dt < 4; ++dt) { const LAS bf16* vp = cb + (16 * dt + fr) * 72 + 32 * p2 + 4 * fq;
;                         o[dt] = __builtin_amdgcn_mfma_f32_16x16x32_bf16(frag44(vp, vp + 16), pf, o[dt], 0, 0, 0); }
;                 }
;             }
;         }
;         if (sidx + 1 < 2 * NCH) NA_STORE(sidx + 1);
;         __syncthreads();
;     }
;     ...
;     lsum += __shfl_xor(lsum, 16); lsum += __shfl_xor(lsum, 32);
	v_mfma_f32_16x16x32_bf16 v[22:25], v[42:45], v[22:25], v[34:37]
	v_ashrrev_i32_e32 v75, 31, v74
	s_nop 1
	v_exp_f32_e32 v34, v6
	v_fma_f32 v6, v18, s71, -v136
	v_mul_f32_e32 v6, 0x3fb8aa3b, v6
	v_exp_f32_e32 v35, v6
	v_fma_f32 v6, v15, s71, -v136
	v_mul_f32_e32 v6, 0x3fb8aa3b, v6
	v_exp_f32_e32 v36, v6
	v_fma_f32 v6, v19, s71, -v136
	v_mul_f32_e32 v6, 0x3fb8aa3b, v6
	v_exp_f32_e32 v37, v6
	v_fma_f32 v6, v16, s71, -v136
	v_mul_f32_e32 v6, 0x3fb8aa3b, v6
	v_exp_f32_e32 v42, v6
	v_fma_f32 v6, v20, s71, -v136
	v_mul_f32_e32 v6, 0x3fb8aa3b, v6
	v_exp_f32_e32 v43, v6
	v_fma_f32 v6, v17, s71, -v136
	v_mul_f32_e32 v14, 0x3fb8aa3b, v6
	ds_read2_b64 v[6:9], v52 offset1:4
	v_exp_f32_e32 v44, v14
	v_fma_f32 v14, v21, s71, -v136
	v_mul_f32_e32 v14, 0x3fb8aa3b, v14
	v_exp_f32_e32 v45, v14
	v_cvt_pk_bf16_f32 v14, v34, v36
	v_cvt_pk_bf16_f32 v15, v42, v44
	v_cvt_pk_bf16_f32 v16, v35, v37
	v_cvt_pk_bf16_f32 v17, v43, v45
	ds_read2_b64 v[18:21], v175 offset0:32 offset1:36
	s_waitcnt lgkmcnt(1)
	v_mfma_f32_16x16x32_bf16 v[6:9], v[6:9], v[14:17], v[26:29]
	s_nop 2
	ds_read2_b64 v[26:29], v176 offset0:64 offset1:68
	s_waitcnt lgkmcnt(0)
	v_mfma_f32_16x16x32_bf16 v[26:29], v[26:29], v[14:17], v[38:41]
	s_nop 2
	v_add_f32_e32 v38, 0, v131
	v_add_f32_e32 v38, v96, v38
	v_add_f32_e32 v38, v95, v38
	v_add_f32_e32 v38, v99, v38
	v_add_f32_e32 v38, v92, v38
	v_add_f32_e32 v38, v91, v38
	v_add_f32_e32 v38, v94, v38
	v_add_f32_e32 v38, v93, v38
	v_add_f32_e32 v38, v86, v38
	v_add_f32_e32 v38, v90, v38
	v_add_f32_e32 v38, v98, v38
	v_add_f32_e32 v38, v100, v38
	v_add_f32_e32 v38, v76, v38
	v_add_f32_e32 v38, v87, v38
	v_add_f32_e32 v38, v97, v38
	v_add_f32_e32 v38, v101, v38
	v_add_f32_e32 v38, v103, v38
	v_add_f32_e32 v38, v105, v38
	v_add_f32_e32 v38, v107, v38
	v_add_f32_e32 v38, v108, v38
	v_add_f32_e32 v38, v102, v38
	v_add_f32_e32 v38, v104, v38
	v_add_f32_e32 v38, v106, v38
	v_add_f32_e32 v38, v109, v38
	v_add_f32_e32 v38, v111, v38
	v_add_f32_e32 v38, v113, v38
	v_add_f32_e32 v38, v115, v38
	v_add_f32_e32 v38, v116, v38
	v_add_f32_e32 v38, v110, v38
	v_add_f32_e32 v38, v112, v38
	v_add_f32_e32 v38, v114, v38
	v_add_f32_e32 v38, v117, v38
	v_add_f32_e32 v38, v119, v38
	v_add_f32_e32 v38, v121, v38
	v_add_f32_e32 v38, v123, v38
	v_add_f32_e32 v38, v124, v38
	v_add_f32_e32 v38, v118, v38
	v_add_f32_e32 v38, v120, v38
	v_add_f32_e32 v38, v122, v38
	v_add_f32_e32 v38, v125, v38
	v_add_f32_e32 v38, v127, v38
	v_add_f32_e32 v38, v129, v38
	v_add_f32_e32 v38, v132, v38
	v_add_f32_e32 v38, v133, v38
	v_add_f32_e32 v38, v126, v38
	v_add_f32_e32 v38, v128, v38
	v_add_f32_e32 v38, v130, v38
	v_add_f32_e32 v38, v134, v38
	v_add_f32_e32 v38, v137, v38
	v_add_f32_e32 v38, v139, v38
	v_add_f32_e32 v38, v141, v38
	v_add_f32_e32 v38, v142, v38
	v_add_f32_e32 v38, v135, v38
	v_add_f32_e32 v38, v138, v38
	v_add_f32_e32 v38, v140, v38
	v_add_f32_e32 v38, v143, v38
	v_add_f32_e32 v38, v78, v38
	v_add_f32_e32 v38, v80, v38
	v_add_f32_e32 v38, v144, v38
	v_add_f32_e32 v38, v146, v38
	v_add_f32_e32 v38, v70, v38
	v_add_f32_e32 v38, v79, v38
	v_add_f32_e32 v38, v81, v38
	v_add_f32_e32 v38, v145, v38
	v_add_f32_e32 v38, v147, v38
	v_add_f32_e32 v38, v66, v38
	v_add_f32_e32 v38, v67, v38
	v_add_f32_e32 v38, v68, v38
	v_add_f32_e32 v38, v62, v38
	v_add_f32_e32 v38, v63, v38
	v_add_f32_e32 v38, v64, v38
	v_add_f32_e32 v38, v65, v38
	v_add_f32_e32 v38, v58, v38
	v_add_f32_e32 v38, v59, v38
	v_add_f32_e32 v38, v60, v38
	v_add_f32_e32 v38, v61, v38
	v_add_f32_e32 v38, v54, v38
	v_add_f32_e32 v38, v55, v38
	v_add_f32_e32 v38, v56, v38
	v_add_f32_e32 v38, v57, v38
	v_add_f32_e32 v38, v69, v38
	v_add_f32_e32 v38, v50, v38
	v_add_f32_e32 v38, v51, v38
	v_add_f32_e32 v38, v174, v38
	v_add_f32_e32 v38, v46, v38
	v_add_f32_e32 v38, v47, v38
	v_add_f32_e32 v38, v48, v38
	v_add_f32_e32 v38, v53, v38
	v_add_f32_e32 v38, v170, v38
	v_mfma_f32_16x16x32_bf16 v[18:21], v[18:21], v[14:17], v[30:33]
	v_add_f32_e32 v38, v172, v38
	v_add_f32_e32 v38, v177, v38
	v_add_f32_e32 v38, v179, v38
	ds_read2_b64 v[30:33], v49 offset0:96 offset1:100
	v_add_f32_e32 v38, v171, v38
	v_add_f32_e32 v38, v173, v38
	v_add_f32_e32 v38, v178, v38
	v_add_f32_e32 v38, v180, v38
	v_add_f32_e32 v38, v162, v38
	v_add_f32_e32 v38, v164, v38
	s_waitcnt lgkmcnt(0)
	v_mfma_f32_16x16x32_bf16 v[14:17], v[30:33], v[14:17], v[22:25]
	v_add_f32_e32 v38, v181, v38
	s_nop 1
	v_exp_f32_e32 v23, v2
	v_fma_f32 v2, v11, s71, -v136
	v_mul_f32_e32 v2, 0x3fb8aa3b, v2
	v_add_f32_e32 v38, v183, v38
	v_exp_f32_e32 v24, v2
	v_fma_f32 v2, v3, s71, -v136
	v_add_f32_e32 v38, v163, v38
	v_mul_f32_e32 v2, 0x3fb8aa3b, v2
	v_add_f32_e32 v38, v165, v38
	v_exp_f32_e32 v25, v2
	v_fma_f32 v2, v12, s71, -v136
	v_add_f32_e32 v38, v182, v38
	v_mul_f32_e32 v2, 0x3fb8aa3b, v2
	v_add_f32_e32 v38, v184, v38
	v_exp_f32_e32 v30, v2
	v_fma_f32 v2, v4, s71, -v136
	v_add_f32_e32 v38, v152, v38
	v_mul_f32_e32 v2, 0x3fb8aa3b, v2
	v_add_f32_e32 v38, v154, v38
	v_exp_f32_e32 v22, v10
	v_exp_f32_e32 v31, v2
	v_fma_f32 v2, v13, s71, -v136
	ds_read2_b64 v[10:13], v52 offset0:8 offset1:12
	v_add_f32_e32 v38, v158, v38
	v_mul_f32_e32 v2, 0x3fb8aa3b, v2
	v_add_f32_e32 v38, v156, v38
	v_exp_f32_e32 v32, v2
	v_fma_f32 v2, v5, s71, -v136
	v_add_f32_e32 v38, v153, v38
	v_mul_f32_e32 v2, 0x3fb8aa3b, v2
	v_add_f32_e32 v38, v155, v38
	v_exp_f32_e32 v33, v2
	v_add_f32_e32 v38, v159, v38
	v_add_f32_e32 v38, v160, v38
	v_add_f32_e32 v34, v34, v38
	v_add_f32_e32 v34, v36, v34
	v_cvt_pk_bf16_f32 v2, v22, v24
	v_cvt_pk_bf16_f32 v3, v30, v32
	v_cvt_pk_bf16_f32 v4, v23, v25
	v_cvt_pk_bf16_f32 v5, v31, v33
	v_add_f32_e32 v34, v42, v34
	v_add_f32_e32 v34, v44, v34
	s_waitcnt lgkmcnt(0)
	v_mfma_f32_16x16x32_bf16 v[6:9], v[10:13], v[2:5], v[6:9]
	ds_read2_b64 v[10:13], v175 offset0:40 offset1:44
	v_add_f32_e32 v34, v35, v34
	v_add_f32_e32 v34, v37, v34
	v_add_f32_e32 v34, v43, v34
	v_add_f32_e32 v34, v45, v34
	v_add_f32_e32 v22, v22, v34
	v_add_f32_e32 v22, v24, v22
	v_add_f32_e32 v22, v30, v22
	v_add_f32_e32 v22, v32, v22
	s_waitcnt lgkmcnt(0)
	v_mfma_f32_16x16x32_bf16 v[10:13], v[10:13], v[2:5], v[18:21]
	v_add_f32_e32 v22, v23, v22
	v_add_f32_e32 v22, v25, v22
	v_add_f32_e32 v22, v31, v22
	ds_read2_b64 v[18:21], v176 offset0:72 offset1:76
	v_add_f32_e32 v30, v33, v22
	ds_bpermute_b32 v31, v88, v30
	ds_read2_b64 v[22:25], v49 offset0:104 offset1:108
	s_waitcnt lgkmcnt(2)
	v_mfma_f32_16x16x32_bf16 v[18:21], v[18:21], v[2:5], v[26:29]
	s_waitcnt lgkmcnt(1)
	s_nop 1
	v_add_f32_e32 v26, v30, v31
	ds_bpermute_b32 v27, v89, v26
	v_lshlrev_b32_e32 v70, 1, v77
	s_waitcnt lgkmcnt(1)
	v_mfma_f32_16x16x32_bf16 v[14:17], v[22:25], v[2:5], v[14:17]
	s_waitcnt lgkmcnt(0)
	s_barrier
; __device__ __forceinline__ unsigned cvt_pk_bf16(float lo, float hi) { const float __attribute__((ext_vector_type(2))) v = {lo, hi}; return __builtin_bit_cast(unsigned, __builtin_convertvector(v, bf16x2_t)); }
; template <bool LOCAL>
; __device__ __forceinline__ void na_unit(const bf16* P, const bf16* VT, bf16* YCAT, const LAS float* rpb_l, LAS bf16* buf, int b, int gr, int hp, int qblk, int tid) {
;     ...
;     lsum += __shfl_xor(lsum, 16); lsum += __shfl_xor(lsum, 32);
;     const float inv = 1.f / lsum;
;     bf16* op = YCAT + (size_t)(qrow0 + fr) * D + 512 + h * 64 + 4 * fq;
; #pragma unroll
;     for (int dt = 0; dt < 4; ++dt) { v2u w; w.x = pg8::cvt_pk_bf16(o[dt][0] * inv, o[dt][1] * inv); w.y = pg8::cvt_pk_bf16(o[dt][2] * inv, o[dt][3] * inv); *(v2u*)(op + dt * 16) = w; }
	v_add_f32_e32 v2, v26, v27
	v_div_scale_f32 v3, s[0:1], v2, v2, 1.0
	v_rcp_f32_e32 v4, v3
	s_nop 0
	v_fma_f32 v5, -v3, v4, 1.0
	v_fmac_f32_e32 v4, v5, v4
	v_div_scale_f32 v5, vcc, 1.0, v2, 1.0
	v_mul_f32_e32 v22, v5, v4
	v_fma_f32 v23, -v3, v22, v5
	v_fmac_f32_e32 v22, v23, v4
	v_fma_f32 v3, -v3, v22, v5
	v_div_fmas_f32 v3, v3, v4, v22
	v_div_fixup_f32 v22, v3, v2, 1.0
	v_lshlrev_b64 v[2:3], 11, v[74:75]
	v_lshl_add_u64 v[2:3], s[10:11], 0, v[2:3]
	v_lshl_add_u64 v[2:3], v[72:73], 1, v[2:3]
	v_pk_mul_f32 v[6:7], v[6:7], v[22:23] op_sel_hi:[1,0]
	v_pk_mul_f32 v[8:9], v[8:9], v[22:23] op_sel_hi:[1,0]
	v_lshl_add_u64 v[4:5], v[2:3], 0, v[70:71]
	v_cvt_pk_bf16_f32 v6, v6, v7
	v_cvt_pk_bf16_f32 v7, v8, v9
	global_store_dwordx2 v[4:5], v[6:7], off offset:1024
	v_pk_mul_f32 v[6:7], v[10:11], v[22:23] op_sel_hi:[1,0]
	v_pk_mul_f32 v[8:9], v[12:13], v[22:23] op_sel_hi:[1,0]
	v_cvt_pk_bf16_f32 v6, v6, v7
	v_cvt_pk_bf16_f32 v7, v8, v9
	global_store_dwordx2 v[4:5], v[6:7], off offset:1056
	v_pk_mul_f32 v[6:7], v[18:19], v[22:23] op_sel_hi:[1,0]
	v_pk_mul_f32 v[8:9], v[20:21], v[22:23] op_sel_hi:[1,0]
	v_cvt_pk_bf16_f32 v6, v6, v7
	v_cvt_pk_bf16_f32 v7, v8, v9
	v_lshl_add_u64 v[2:3], v[4:5], 0, s[12:13]
	global_store_dwordx2 v[4:5], v[6:7], off offset:1088
	v_pk_mul_f32 v[4:5], v[14:15], v[22:23] op_sel_hi:[1,0]
	v_pk_mul_f32 v[6:7], v[16:17], v[22:23] op_sel_hi:[1,0]
	v_cvt_pk_bf16_f32 v4, v4, v5

; #define LAS __attribute__((address_space(3)))
; template <bool LOCAL>
; __device__ __forceinline__ void na_unit(const bf16* P, const bf16* VT, bf16* YCAT, const LAS float* rpb_l, LAS bf16* buf, int b, int gr, int hp, int qblk, int tid) {
;     typedef pg8::bf16x8 bf16x8;
;     constexpr int NCH = LOCAL ? 12 : 4, NLOC = LOCAL ? 8 : 0;
;     const int lane = tid & 63, wv = tid >> 6, fr = lane & 15, fq = lane >> 4, hh = wv >> 2, qb = wv & 3, h = 2 * hp + hh;
;     const int qrow0 = LOCAL ? NCTX + b * SEQ + gr * 64 + 16 * qb : b * CTXL + qblk * 64 + 16 * qb;
;     const int r0 = min(max(gr - 4, 0), 24);
;     const int kc0 = qb == 0 ? 0 : qb == 1 ? 8 : qb == 2 ? 24 : 32;
;     const int qcol = 16 * qb + fr, cs = min(max(qcol - 8, 0), 48);
;     const LAS float* rpb = rpb_l + h * 15 * 31;
;     v4u ld[2][2];
;     const int lrow = (tid >> 3) & 63, lseg = tid & 7;
;     ...
;     bf16x8 qf[2];
; #pragma unroll
;     for (int ks = 0; ks < 2; ++ks) qf[ks] = *(const bf16x8*)(P + (size_t)(qrow0 + fr) * DINP + h * 64 + 32 * ks + 8 * fq);
;     f32x4 sl[16], sc[16];
;     float m = -1.0e30f, lsum = 0.f;
;     f32x4 o[4];
; #pragma unroll
;     for (int dt = 0; dt < 4; ++dt) o[dt] = (f32x4){0.f, 0.f, 0.f, 0.f};
;     NA_ISSUE(0); NA_ISSUE(1); NA_STORE(0);
;     __syncthreads();
; #pragma unroll
;     for (int sidx = 0; sidx < 2 * NCH; ++sidx) {
;         if (sidx + 2 < 2 * NCH) NA_ISSUE(sidx + 2);
;         const LAS bf16* cb = buf + (sidx & 1) * 9216 + hh * 4608;
;         if (sidx < NCH) {
;             const int c = sidx;
;             if (LOCAL && c < 8) {
; #pragma unroll
;                 for (int t2 = 0; t2 < 2; ++t2) {
;                     const LAS bf16* kp = cb + (kc0 + 16 * t2 + fr) * 72 + 8 * fq;
;                     f32x4 acc = {0.f, 0.f, 0.f, 0.f};
;                     acc = __builtin_amdgcn_mfma_f32_16x16x32_bf16(*(const LAS bf16x8*)(kp), qf[0], acc, 0, 0, 0);
;                     acc = __builtin_amdgcn_mfma_f32_16x16x32_bf16(*(const LAS bf16x8*)(kp + 32), qf[1], acc, 0, 0, 0);
;                     const LAS float* rb = rpb + (r0 + c - gr + 7) * 31 + 15 - qcol;
; #pragma unroll
;                     for (int e = 0; e < 4; ++e) { const int kcol = kc0 + 16 * t2 + 4 * fq + e; const bool ok = (kcol >= cs) && (kcol < cs + 16);
;                         const float sv = ok ? acc[e] * 0.125f + rb[ok ? kcol : qcol] : -1.0e30f; acc[e] = sv; m = fmaxf(m, sv); }
.LBB0_1737:
	v_mov_b32_e32 v92, v0
	s_movk_i32 s2, 0x2400
	v_and_b32_e32 v88, 15, v92
	v_bfe_u32 v90, v92, 4, 2
	v_ashrrev_i32_e32 v91, 8, v92
	s_mov_b64 s[0:1], -1
	s_cmpk_gt_i32 s75, 0x7ff
	v_bfe_u32 v87, v92, 3, 6
	v_lshlrev_b32_e32 v76, 3, v90
	v_lshlrev_b32_e32 v70, 4, v90
	v_mad_i32_i24 v85, v91, s2, 0
	v_mul_u32_u24_e32 v86, 0x90, v88
	s_waitcnt lgkmcnt(0)
	s_barrier
	s_cbranch_scc0 .LBB0_1739
	s_lshl_b32 s0, s75, 4
	s_and_b32 s0, s0, 0xffffff00
	s_addk_i32 s0, 0x8000
	v_mov_b64_e32 v[78:79], s[8:9]
	s_lshl_b32 s1, s75, 5
	v_or_b32_e32 v77, s0, v87
	v_lshlrev_b32_e32 v4, 4, v92
	s_and_b32 s16, s1, 0x180
	v_mad_u64_u32 v[2:3], s[14:15], v77, s69, v[78:79]
	v_and_b32_e32 v80, 0x70, v4
	v_mov_b32_e32 v81, v71
	v_lshl_add_u64 v[2:3], v[2:3], 0, v[80:81]
	s_lshl_b32 s2, s16, 1
	v_lshl_add_u64 v[2:3], v[2:3], 0, s[2:3]
	global_load_dwordx4 v[6:9], v[2:3], off offset:1024
	global_load_dwordx4 v[10:13], v[2:3], off offset:1152
	s_lshl_b32 s1, s75, 6
	s_and_b32 s1, s1, 0xc0
	v_lshrrev_b32_e32 v2, 2, v92
	v_and_or_b32 v2, v2, 48, s1
	v_lshl_add_u32 v4, v91, 6, s16
	v_or3_b32 v72, v2, v88, s0
	v_ashrrev_i32_e32 v5, 31, v4
	v_mad_u64_u32 v[2:3], s[14:15], v72, s69, v[78:79]
	v_lshlrev_b64 v[74:75], 1, v[4:5]
	v_lshl_add_u64 v[2:3], v[2:3], 0, v[74:75]
	v_or_b32_e32 v14, 64, v77
	v_lshl_add_u64 v[22:23], v[2:3], 0, v[70:71]
	v_mad_u64_u32 v[14:15], s[14:15], v14, s69, v[78:79]
	global_load_dwordx4 v[2:5], v[22:23], off
	v_lshl_add_u64 v[14:15], v[14:15], 0, v[80:81]
	v_lshl_add_u64 v[18:19], v[14:15], 0, s[2:3]
	s_mov_b32 s100, 0x60000
	s_mov_b32 s101, 0
	v_lshl_add_u64 v[248:249], v[18:19], 0, s[100:101]
	global_load_dwordx4 v[14:17], v[18:19], off offset:1024
	s_nop 0
	global_load_dwordx4 v[18:21], v[18:19], off offset:1152
	global_load_dword v250, v[248:249], off offset:1024
	global_load_dword v251, v[248:249], off offset:1152
	s_nop 0
	global_load_dwordx4 v[50:53], v[22:23], off offset:64
	v_mul_u32_u24_e32 v22, 0x90, v87
	v_add3_u32 v73, 0, v22, v80
	v_or_b32_e32 v22, 0x80, v77
	v_add3_u32 v89, v85, v70, v86
	s_mov_b32 s1, s3
	v_cmp_lt_i32_e32 vcc, v82, v83
	s_waitcnt vmcnt(7)
	ds_write_b128 v73, v[6:9]
	s_waitcnt vmcnt(6)
	ds_write_b128 v73, v[10:13] offset:9216
	v_mad_u64_u32 v[10:11], s[14:15], v22, s69, v[78:79]
	v_lshl_add_u64 v[10:11], v[10:11], 0, v[80:81]
	v_lshl_add_u64 v[26:27], v[10:11], 0, s[2:3]
	s_waitcnt lgkmcnt(0)
	s_barrier
	ds_read_b128 v[6:9], v89
	ds_read_b128 v[10:13], v89 offset:2304
	v_lshl_add_u64 v[248:249], v[26:27], 0, s[100:101]
	global_load_dwordx4 v[22:25], v[26:27], off offset:1024
	global_load_dwordx4 v[30:33], v[26:27], off offset:1152
	global_load_dword v250, v[248:249], off offset:1024
	global_load_dword v251, v[248:249], off offset:1152
	ds_read_b128 v[26:29], v89 offset:64
	ds_read_b128 v[34:37], v89 offset:4608
	ds_read_b128 v[38:41], v89 offset:2368
	ds_read_b128 v[42:45], v89 offset:4672
	ds_read_b128 v[46:49], v89 offset:6912
	s_waitcnt vmcnt(9) lgkmcnt(6)
	v_mfma_f32_16x16x32_bf16 v[6:9], v[6:9], v[2:5], 0
	ds_read_b128 v[54:57], v89 offset:6976
	s_waitcnt vmcnt(8)
	ds_write_b128 v73, v[14:17] offset:18432
	s_waitcnt vmcnt(7)
	ds_write_b128 v73, v[18:21] offset:27648
	s_waitcnt lgkmcnt(0)
	v_mfma_f32_16x16x32_bf16 v[10:13], v[10:13], v[2:5], 0
	s_barrier
	v_mfma_f32_16x16x32_bf16 v[14:17], v[34:37], v[2:5], 0
	v_mfma_f32_16x16x32_bf16 v[18:21], v[46:49], v[2:5], 0
	ds_read_b128 v[34:37], v89 offset:18432
	ds_read_b128 v[46:49], v89 offset:18496
	ds_read_b128 v[58:61], v89 offset:20736
	ds_read_b128 v[94:97], v89 offset:20800
	s_waitcnt vmcnt(4)
	v_mfma_f32_16x16x32_bf16 v[62:65], v[26:29], v[50:53], v[6:9]
	s_nop 2
	v_or_b32_e32 v6, s16, v87
	s_waitcnt lgkmcnt(1)
	v_mfma_f32_16x16x32_bf16 v[98:101], v[58:61], v[2:5], 0
	ds_read_b128 v[58:61], v89 offset:23040
	ds_read_b128 v[102:105], v89 offset:23104
	v_mul_u32_u24_e32 v8, 0x9000, v6
	v_mov_b32_e32 v7, v71
	v_mfma_f32_16x16x32_bf16 v[66:69], v[38:41], v[50:53], v[10:13]
	v_mov_b32_e32 v9, v71
	s_nop 1
	v_lshl_add_u64 v[10:11], s[4:5], 0, v[80:81]
	v_or_b32_e32 v12, 64, v6
	v_or_b32_e32 v13, 0xc0, v77
	v_lshl_add_u64 v[10:11], s[0:1], 1, v[10:11]
	v_lshlrev_b32_e32 v6, 1, v8
	v_mul_u32_u24_e32 v8, 0x9000, v12
	v_mad_u64_u32 v[12:13], s[0:1], v13, s69, v[78:79]
	v_lshl_add_u64 v[78:79], v[10:11], 0, v[6:7]
	v_lshlrev_b32_e32 v8, 1, v8
	v_lshl_add_u64 v[6:7], v[12:13], 0, v[80:81]
	v_lshl_add_u64 v[80:81], v[10:11], 0, v[8:9]
	v_lshl_add_u64 v[10:11], v[6:7], 0, s[2:3]
	s_waitcnt lgkmcnt(1)
	v_mfma_f32_16x16x32_bf16 v[106:109], v[58:61], v[2:5], 0
	ds_read_b128 v[58:61], v89 offset:25344
	ds_read_b128 v[110:113], v89 offset:25408
	global_load_dwordx4 v[6:9], v[10:11], off offset:1024
	s_nop 0
	global_load_dwordx4 v[10:13], v[10:11], off offset:1152
	v_mul_f32_e32 v38, 0x3e000000, v68
	s_waitcnt lgkmcnt(1)
	v_mfma_f32_16x16x32_bf16 v[114:117], v[58:61], v[2:5], 0
	v_mul_f32_e32 v39, 0x3e000000, v69
	s_waitcnt vmcnt(5)
	ds_write_b128 v73, v[22:25]
	s_waitcnt vmcnt(4)
	ds_write_b128 v73, v[30:33] offset:9216
	v_mfma_f32_16x16x32_bf16 v[58:61], v[42:45], v[50:53], v[14:17]
	s_waitcnt lgkmcnt(0)
	s_barrier
; #define LAS __attribute__((address_space(3)))
; template <bool LOCAL>
; __device__ __forceinline__ void na_unit(const bf16* P, const bf16* VT, bf16* YCAT, const LAS float* rpb_l, LAS bf16* buf, int b, int gr, int hp, int qblk, int tid) {
;     ...
;             } else {
;                 const int cc = c - NLOC;
; #pragma unroll
;                 for (int t4 = 0; t4 < 4; ++t4) {
;                     const LAS bf16* kp = cb + (16 * t4 + fr) * 72 + 8 * fq;
;                     f32x4 acc = {0.f, 0.f, 0.f, 0.f};
;                     acc = __builtin_amdgcn_mfma_f32_16x16x32_bf16(*(const LAS bf16x8*)(kp), qf[0], acc, 0, 0, 0);
;                     acc = __builtin_amdgcn_mfma_f32_16x16x32_bf16(*(const LAS bf16x8*)(kp + 32), qf[1], acc, 0, 0, 0);
; #pragma unroll
;                     for (int e = 0; e < 4; ++e) { acc[e] *= 0.125f; m = fmaxf(m, acc[e]); }
;                     sc[4 * (cc >= 0 ? cc : 0) + t4] = acc; }
;             }
;             if (sidx == NCH - 1) { m = fmaxf(m, __shfl_xor(m, 16)); m = fmaxf(m, __shfl_xor(m, 32)); }
;         } else {
;             const int c = sidx - NCH;
;             if (LOCAL && c < 8) {
;                 float p[8];
; #pragma unroll
;                 for (int e = 0; e < 4; ++e) { p[e] = __expf(sl[2 * (c < 8 ? c : 0)][e] - m); p[4 + e] = __expf(sl[2 * (c < 8 ? c : 0) + 1][e] - m); }
; #pragma unroll
;                 for (int e = 0; e < 8; ++e) lsum += p[e];
;                 const bf16x8 pf = __builtin_bit_cast(bf16x8, (v4u){pg8::cvt_pk_bf16(p[0], p[1]), pg8::cvt_pk_bf16(p[2], p[3]), pg8::cvt_pk_bf16(p[4], p[5]), pg8::cvt_pk_bf16(p[6], p[7])});
; #pragma unroll
;                 for (int dt = 0; dt < 4; ++dt) { const LAS bf16* vp = cb + (16 * dt + fr) * 72 + kc0 + 4 * fq;
;                     o[dt] = __builtin_amdgcn_mfma_f32_16x16x32_bf16(frag44(vp, vp + 16), pf, o[dt], 0, 0, 0); }
;             } else {
;                 const int cc = c - NLOC;
; #pragma unroll
;                 for (int p2 = 0; p2 < 2; ++p2) {
;                     float p[8];
; #pragma unroll
;                     for (int e = 0; e < 4; ++e) { p[e] = __expf(sc[4 * (cc >= 0 ? cc : 0) + 2 * p2][e] - m); p[4 + e] = __expf(sc[4 * (cc >= 0 ? cc : 0) + 2 * p2 + 1][e] - m); }
; #pragma unroll
;                     for (int e = 0; e < 8; ++e) lsum += p[e];
	s_nop 0
	v_mul_f32_e32 v14, 0x3e000000, v62
	v_mul_f32_e32 v15, 0x3e000000, v63
	v_mfma_f32_16x16x32_bf16 v[54:57], v[54:57], v[50:53], v[18:21]
	s_nop 1
	v_mul_f32_e32 v40, 0x3e000000, v58
	v_mul_f32_e32 v41, 0x3e000000, v59
	v_mul_f32_e32 v77, 0x3e000000, v60
	v_mfma_f32_16x16x32_bf16 v[42:45], v[94:97], v[50:53], v[98:101]
	v_mul_f32_e32 v18, 0x3e000000, v64
	v_mul_f32_e32 v19, 0x3e000000, v65
	v_mul_f32_e32 v20, 0x3e000000, v66
	v_max3_f32 v98, v14, s74, v15
	v_mul_f32_e32 v21, 0x3e000000, v67
	v_max3_f32 v18, v98, v18, v19
	v_mfma_f32_16x16x32_bf16 v[34:37], v[34:37], v[2:5], 0
	v_max3_f32 v18, v18, v20, v21
	ds_read_b128 v[14:17], v89
	v_max3_f32 v22, v18, v38, v39
	ds_read_b128 v[18:21], v89 offset:2304
	v_mul_f32_e32 v93, 0x3e000000, v61
	v_max3_f32 v22, v22, v40, v41
	v_mul_f32_e32 v94, 0x3e000000, v54
	v_mul_f32_e32 v95, 0x3e000000, v55
	v_max3_f32 v38, v22, v77, v93
	v_mfma_f32_16x16x32_bf16 v[46:49], v[46:49], v[50:53], v[34:37]
	v_mul_f32_e32 v96, 0x3e000000, v56
	v_mul_f32_e32 v97, 0x3e000000, v57
	v_max3_f32 v38, v38, v94, v95
	ds_read_b128 v[22:25], v89 offset:64
	ds_read_b128 v[30:33], v89 offset:4608
	v_max3_f32 v38, v38, v96, v97
	ds_read_b128 v[94:97], v89 offset:2368
	v_mfma_f32_16x16x32_bf16 v[34:37], v[102:105], v[50:53], v[106:109]
	v_mul_f32_e32 v99, 0x3e000000, v46
	v_mul_f32_e32 v100, 0x3e000000, v47
	v_mul_f32_e32 v101, 0x3e000000, v48
	v_mul_f32_e32 v102, 0x3e000000, v49
	v_max3_f32 v38, v38, v99, v100
	v_mul_f32_e32 v106, 0x3e000000, v42
	v_mul_f32_e32 v107, 0x3e000000, v43
	s_waitcnt lgkmcnt(4)
	v_mfma_f32_16x16x32_bf16 v[14:17], v[14:17], v[2:5], 0
	v_max3_f32 v38, v38, v101, v102
	v_mul_f32_e32 v108, 0x3e000000, v44
	v_mul_f32_e32 v109, 0x3e000000, v45
	s_waitcnt lgkmcnt(3)
	v_mfma_f32_16x16x32_bf16 v[18:21], v[18:21], v[2:5], 0
	ds_read_b128 v[98:101], v89 offset:4672
	s_waitcnt lgkmcnt(2)
	v_mfma_f32_16x16x32_bf16 v[102:105], v[30:33], v[2:5], 0
	v_max3_f32 v30, v38, v106, v107
	v_max3_f32 v30, v30, v108, v109
	v_mfma_f32_16x16x32_bf16 v[26:29], v[110:113], v[50:53], v[114:117]
	v_mul_f32_e32 v110, 0x3e000000, v34
	v_mul_f32_e32 v111, 0x3e000000, v35
	v_mul_f32_e32 v112, 0x3e000000, v36
	v_mul_f32_e32 v113, 0x3e000000, v37
	v_max3_f32 v30, v30, v110, v111
	v_mfma_f32_16x16x32_bf16 v[38:41], v[22:25], v[50:53], v[14:17]
	s_nop 1
	v_mul_f32_e32 v114, 0x3e000000, v26
	v_mul_f32_e32 v115, 0x3e000000, v27
	v_mul_f32_e32 v116, 0x3e000000, v28
	v_max3_f32 v14, v30, v112, v113
	s_waitcnt lgkmcnt(1)
	v_mfma_f32_16x16x32_bf16 v[30:33], v[94:97], v[50:53], v[18:21]
	v_lshl_add_u64 v[248:249], v[78:79], 0, 0
	v_lshl_add_u64 v[238:239], v[80:81], 0, 0
	global_load_dwordx4 v[94:97], v[78:79], off
	global_load_dwordx4 v[106:109], v[80:81], off
	global_load_dword v250, v[248:249], off offset:128
	global_load_dword v251, v[238:239], off offset:128
	v_mul_f32_e32 v117, 0x3e000000, v29
	v_max3_f32 v14, v14, v114, v115
	v_max3_f32 v22, v14, v116, v117
	ds_read_b128 v[14:17], v89 offset:6912
	v_mul_f32_e32 v23, 0x3e000000, v38
	v_mul_f32_e32 v24, 0x3e000000, v39
	v_mul_f32_e32 v25, 0x3e000000, v40
	v_mul_f32_e32 v77, 0x3e000000, v41
	v_max3_f32 v22, v22, v23, v24
	s_waitcnt lgkmcnt(1)
	v_mfma_f32_16x16x32_bf16 v[18:21], v[98:101], v[50:53], v[102:105]
	v_mul_f32_e32 v93, 0x3e000000, v30
	v_mul_f32_e32 v98, 0x3e000000, v31
	v_max3_f32 v22, v22, v25, v77
	v_max3_f32 v77, v22, v93, v98
	ds_read_b128 v[22:25], v89 offset:6976
	s_waitcnt vmcnt(5)
	ds_write_b128 v73, v[6:9] offset:18432
	s_waitcnt vmcnt(4)
	ds_write_b128 v73, v[10:13] offset:27648
	s_waitcnt lgkmcnt(0)
	s_barrier
	ds_read_b128 v[6:9], v89 offset:18432
	v_mul_f32_e32 v99, 0x3e000000, v32
	v_mul_f32_e32 v10, 0x3e000000, v33
	v_mfma_f32_16x16x32_bf16 v[14:17], v[14:17], v[2:5], 0
	v_max3_f32 v77, v77, v99, v10
	ds_read_b128 v[10:13], v89 offset:18496
	v_mul_f32_e32 v93, 0x3e000000, v18
	v_mfma_f32_16x16x32_bf16 v[22:25], v[22:25], v[50:53], v[14:17]
	v_mul_f32_e32 v98, 0x3e000000, v21
	ds_read_b128 v[110:113], v89 offset:25408
	s_nop 1
	v_mul_f32_e32 v14, 0x3e000000, v19
	v_max3_f32 v77, v77, v93, v14
	s_waitcnt lgkmcnt(2)
	v_mfma_f32_16x16x32_bf16 v[6:9], v[6:9], v[2:5], 0
	ds_read_b128 v[14:17], v89 offset:20736
	v_mul_f32_e32 v93, 0x3e000000, v20
	v_max3_f32 v77, v77, v93, v98
	s_waitcnt lgkmcnt(2)
	v_mfma_f32_16x16x32_bf16 v[10:13], v[10:13], v[50:53], v[6:9]
	v_mul_f32_e32 v93, 0x3e000000, v22
	v_mul_f32_e32 v98, 0x3e000000, v23
	v_max3_f32 v77, v77, v93, v98
	ds_read_b128 v[6:9], v89 offset:20800
	s_waitcnt lgkmcnt(1)
	v_mfma_f32_16x16x32_bf16 v[14:17], v[14:17], v[2:5], 0
	ds_read_b128 v[98:101], v89 offset:23040
	v_mul_f32_e32 v93, 0x3e000000, v24
	v_mul_f32_e32 v102, 0x3e000000, v25
	s_waitcnt lgkmcnt(1)
	v_mfma_f32_16x16x32_bf16 v[14:17], v[6:9], v[50:53], v[14:17]
	ds_read_b128 v[6:9], v89 offset:23104
	v_max3_f32 v77, v77, v93, v102
	ds_read_b128 v[102:105], v89 offset:25344
	s_waitcnt lgkmcnt(2)
	v_mfma_f32_16x16x32_bf16 v[98:101], v[98:101], v[2:5], 0
	v_mul_f32_e32 v93, 0x3e000000, v10
	v_mul_f32_e32 v114, 0x3e000000, v11
	v_mul_f32_e32 v115, 0x3e000000, v12
	s_waitcnt lgkmcnt(1)
	v_mfma_f32_16x16x32_bf16 v[6:9], v[6:9], v[50:53], v[98:101]
	v_mul_f32_e32 v116, 0x3e000000, v13
	v_max3_f32 v77, v77, v93, v114
	v_mul_f32_e32 v117, 0x3e000000, v14
	v_mul_f32_e32 v118, 0x3e000000, v15
	s_waitcnt lgkmcnt(0)
	v_mfma_f32_16x16x32_bf16 v[2:5], v[102:105], v[2:5], 0
	v_max3_f32 v77, v77, v115, v116
	v_mul_f32_e32 v89, 0x3e000000, v16
	v_mul_f32_e32 v98, 0x3e000000, v17
	v_max3_f32 v77, v77, v117, v118
	v_mul_f32_e32 v99, 0x3e000000, v6
	v_mul_f32_e32 v100, 0x3e000000, v7
	v_max3_f32 v77, v77, v89, v98
	v_mul_f32_e32 v101, 0x3e000000, v8
	v_mul_f32_e32 v102, 0x3e000000, v9
	v_max3_f32 v77, v77, v99, v100
	v_mfma_f32_16x16x32_bf16 v[2:5], v[110:113], v[50:53], v[2:5]
	v_max3_f32 v77, v77, v101, v102
	v_lshl_add_u64 v[248:249], v[78:79], 0, 0
	v_lshl_add_u64 v[238:239], v[80:81], 0, 0
	global_load_dwordx4 v[98:101], v[78:79], off offset:128
	global_load_dwordx4 v[102:105], v[80:81], off offset:128
	global_load_dword v250, v[248:249], off offset:256
	global_load_dword v251, v[238:239], off offset:256
	s_waitcnt vmcnt(7)
	ds_write_b128 v73, v[94:97]
	s_waitcnt vmcnt(6)
	ds_write_b128 v73, v[106:109] offset:9216
	s_nop 0
	v_mul_f32_e32 v50, 0x3e000000, v2
	v_mul_f32_e32 v51, 0x3e000000, v3
	v_mul_f32_e32 v52, 0x3e000000, v4
	v_mul_f32_e32 v53, 0x3e000000, v5
	v_max3_f32 v50, v77, v50, v51
	v_max3_f32 v51, v50, v52, v53
	v_cndmask_b32_e32 v50, v1, v82, vcc
	v_lshlrev_b32_e32 v50, 2, v50
	ds_bpermute_b32 v52, v50, v51
	v_cmp_lt_i32_e32 vcc, v84, v83
	s_waitcnt lgkmcnt(0)
	s_barrier
; #define LAS __attribute__((address_space(3)))
; __device__ __forceinline__ unsigned cvt_pk_bf16(float lo, float hi) { const float __attribute__((ext_vector_type(2))) v = {lo, hi}; return __builtin_bit_cast(unsigned, __builtin_convertvector(v, bf16x2_t)); }
; template <bool LOCAL>
; __device__ __forceinline__ void na_unit(const bf16* P, const bf16* VT, bf16* YCAT, const LAS float* rpb_l, LAS bf16* buf, int b, int gr, int hp, int qblk, int tid) {
;     ...
;             if (sidx == NCH - 1) { m = fmaxf(m, __shfl_xor(m, 16)); m = fmaxf(m, __shfl_xor(m, 32)); }
;         } else {
;             const int c = sidx - NCH;
;             if (LOCAL && c < 8) {
;                 float p[8];
; #pragma unroll
;                 for (int e = 0; e < 4; ++e) { p[e] = __expf(sl[2 * (c < 8 ? c : 0)][e] - m); p[4 + e] = __expf(sl[2 * (c < 8 ? c : 0) + 1][e] - m); }
; #pragma unroll
;                 for (int e = 0; e < 8; ++e) lsum += p[e];
;                 const bf16x8 pf = __builtin_bit_cast(bf16x8, (v4u){pg8::cvt_pk_bf16(p[0], p[1]), pg8::cvt_pk_bf16(p[2], p[3]), pg8::cvt_pk_bf16(p[4], p[5]), pg8::cvt_pk_bf16(p[6], p[7])});
; #pragma unroll
;                 for (int dt = 0; dt < 4; ++dt) { const LAS bf16* vp = cb + (16 * dt + fr) * 72 + kc0 + 4 * fq;
;                     o[dt] = __builtin_amdgcn_mfma_f32_16x16x32_bf16(frag44(vp, vp + 16), pf, o[dt], 0, 0, 0); }
;             } else {
;                 const int cc = c - NLOC;
; #pragma unroll
;                 for (int p2 = 0; p2 < 2; ++p2) {
;                     float p[8];
; #pragma unroll
;                     for (int e = 0; e < 4; ++e) { p[e] = __expf(sc[4 * (cc >= 0 ? cc : 0) + 2 * p2][e] - m); p[4 + e] = __expf(sc[4 * (cc >= 0 ? cc : 0) + 2 * p2 + 1][e] - m); }
; #pragma unroll
;                     for (int e = 0; e < 8; ++e) lsum += p[e];
;                     const bf16x8 pf = __builtin_bit_cast(bf16x8, (v4u){pg8::cvt_pk_bf16(p[0], p[1]), pg8::cvt_pk_bf16(p[2], p[3]), pg8::cvt_pk_bf16(p[4], p[5]), pg8::cvt_pk_bf16(p[6], p[7])});
; #pragma unroll
;                     for (int dt = 0; dt < 4; ++dt) { const LAS bf16* vp = cb + (16 * dt + fr) * 72 + 32 * p2 + 4 * fq;
;                         o[dt] = __builtin_amdgcn_mfma_f32_16x16x32_bf16(frag44(vp, vp + 16), pf, o[dt], 0, 0, 0); }
;                 }
;             }
;         }
;         if (sidx + 1 < 2 * NCH) NA_STORE(sidx + 1);
	v_max_f32_e32 v52, v52, v52
	v_max_f32_e32 v52, v51, v52
	v_cndmask_b32_e32 v51, v1, v84, vcc
	v_lshlrev_b32_e32 v51, 2, v51
	ds_bpermute_b32 v53, v51, v52
	s_waitcnt lgkmcnt(0)
	v_max_f32_e32 v53, v53, v53
	v_max_f32_e32 v77, v52, v53
	v_fma_f32 v52, v62, s71, -v77
	v_fma_f32 v64, v64, s71, -v77
	v_mul_f32_e32 v52, 0x3fb8aa3b, v52
	v_fma_f32 v62, v63, s71, -v77
	v_mul_f32_e32 v64, 0x3fb8aa3b, v64
	v_fma_f32 v65, v65, s71, -v77
	v_exp_f32_e32 v53, v52
	v_fma_f32 v52, v66, s71, -v77
	v_mul_f32_e32 v62, 0x3fb8aa3b, v62
	v_exp_f32_e32 v66, v64
	v_fma_f32 v64, v68, s71, -v77
	v_mul_f32_e32 v65, 0x3fb8aa3b, v65
	v_add3_u32 v68, v85, v76, v86
	v_exp_f32_e32 v63, v62
	v_fma_f32 v62, v67, s71, -v77
	v_exp_f32_e32 v67, v65
	v_fma_f32 v65, v69, s71, -v77
	v_add_u32_e32 v69, 0x800, v68
	v_add_u32_e32 v89, 0x1000, v68
	v_add_u32_e32 v93, 0x1800, v68
	ds_read2_b64 v[94:97], v68 offset1:4
	ds_read2_b64 v[110:113], v69 offset0:32 offset1:36
	ds_read2_b64 v[114:117], v89 offset0:64 offset1:68
	ds_read2_b64 v[118:121], v93 offset0:96 offset1:100
	v_mul_f32_e32 v52, 0x3fb8aa3b, v52
	v_mul_f32_e32 v62, 0x3fb8aa3b, v62
	v_mul_f32_e32 v64, 0x3fb8aa3b, v64
	v_mul_f32_e32 v65, 0x3fb8aa3b, v65
	v_exp_f32_e32 v52, v52
	v_exp_f32_e32 v62, v62
	v_exp_f32_e32 v64, v64
	v_exp_f32_e32 v65, v65
	v_cvt_pk_bf16_f32 v106, v53, v63
	v_cvt_pk_bf16_f32 v107, v66, v67
	v_cvt_pk_bf16_f32 v108, v52, v62
	v_cvt_pk_bf16_f32 v109, v64, v65
	v_fma_f32 v58, v58, s71, -v77
	v_fma_f32 v54, v54, s71, -v77
	s_waitcnt lgkmcnt(3)
	v_mfma_f32_16x16x32_bf16 v[94:97], v[94:97], v[106:109], 0
	v_fma_f32 v59, v59, s71, -v77
	v_fma_f32 v55, v55, s71, -v77
	v_fma_f32 v60, v60, s71, -v77
	s_waitcnt lgkmcnt(2)
	v_mfma_f32_16x16x32_bf16 v[110:113], v[110:113], v[106:109], 0
	v_fma_f32 v56, v56, s71, -v77
	v_fma_f32 v61, v61, s71, -v77
	v_fma_f32 v57, v57, s71, -v77
	s_waitcnt lgkmcnt(1)
	v_mfma_f32_16x16x32_bf16 v[114:117], v[114:117], v[106:109], 0
	v_mul_f32_e32 v58, 0x3fb8aa3b, v58
	v_mul_f32_e32 v54, 0x3fb8aa3b, v54
	v_mul_f32_e32 v59, 0x3fb8aa3b, v59
	s_waitcnt lgkmcnt(0)
	v_mfma_f32_16x16x32_bf16 v[106:109], v[118:121], v[106:109], 0
	ds_read2_b64 v[118:121], v68 offset0:8 offset1:12
	v_mul_f32_e32 v55, 0x3fb8aa3b, v55
	v_mul_f32_e32 v60, 0x3fb8aa3b, v60
	v_mul_f32_e32 v56, 0x3fb8aa3b, v56
	v_mul_f32_e32 v61, 0x3fb8aa3b, v61
	v_mul_f32_e32 v57, 0x3fb8aa3b, v57
	v_exp_f32_e32 v58, v58
	v_exp_f32_e32 v54, v54
	v_exp_f32_e32 v59, v59
	v_exp_f32_e32 v55, v55
	v_exp_f32_e32 v60, v60
	v_exp_f32_e32 v56, v56
	v_exp_f32_e32 v61, v61
	v_exp_f32_e32 v57, v57
	v_cvt_pk_bf16_f32 v122, v58, v59
	v_cvt_pk_bf16_f32 v124, v54, v55
	v_cvt_pk_bf16_f32 v123, v60, v61
	v_cvt_pk_bf16_f32 v125, v56, v57
	v_fma_f32 v42, v42, s71, -v77
	v_mul_f32_e32 v42, 0x3fb8aa3b, v42
	s_waitcnt lgkmcnt(0)
	v_mfma_f32_16x16x32_bf16 v[94:97], v[118:121], v[122:125], v[94:97]
	ds_read2_b64 v[118:121], v69 offset0:40 offset1:44
	v_fma_f32 v46, v46, s71, -v77
	v_mul_f32_e32 v46, 0x3fb8aa3b, v46
	s_waitcnt lgkmcnt(0)
	v_mfma_f32_16x16x32_bf16 v[110:113], v[118:121], v[122:125], v[110:113]
	ds_read2_b64 v[118:121], v89 offset0:72 offset1:76
	v_add_u32_e32 v135, 0x5000, v68
	v_fma_f32 v26, v26, s71, -v77
	s_waitcnt lgkmcnt(0)
	v_mfma_f32_16x16x32_bf16 v[114:117], v[118:121], v[122:125], v[114:117]
	ds_read2_b64 v[118:121], v93 offset0:104 offset1:108
	v_lshl_add_u64 v[248:249], v[78:79], 0, 0
	v_lshl_add_u64 v[238:239], v[80:81], 0, 0
	global_load_dwordx4 v[126:129], v[78:79], off offset:256
	global_load_dwordx4 v[130:133], v[80:81], off offset:256
	global_load_dword v250, v[248:249], off offset:384
	global_load_dword v251, v[238:239], off offset:384
	s_waitcnt vmcnt(7)
	ds_write_b128 v73, v[98:101] offset:18432
	s_waitcnt vmcnt(6)
	ds_write_b128 v73, v[102:105] offset:27648
	s_waitcnt lgkmcnt(2)
	v_mfma_f32_16x16x32_bf16 v[106:109], v[118:121], v[122:125], v[106:109]
	v_exp_f32_e32 v119, v42
	v_fma_f32 v42, v47, s71, -v77
	v_mul_f32_e32 v42, 0x3fb8aa3b, v42
	v_exp_f32_e32 v120, v42
	v_fma_f32 v42, v43, s71, -v77
	v_mul_f32_e32 v42, 0x3fb8aa3b, v42
	v_exp_f32_e32 v121, v42
	v_fma_f32 v42, v48, s71, -v77
	v_mul_f32_e32 v42, 0x3fb8aa3b, v42
	v_exp_f32_e32 v122, v42
	v_fma_f32 v42, v44, s71, -v77
	v_mul_f32_e32 v42, 0x3fb8aa3b, v42
	v_add_u32_e32 v124, 0x4800, v68
	s_waitcnt lgkmcnt(0)
	s_barrier
; #define LAS __attribute__((address_space(3)))
; __device__ __forceinline__ unsigned cvt_pk_bf16(float lo, float hi) { const float __attribute__((ext_vector_type(2))) v = {lo, hi}; return __builtin_bit_cast(unsigned, __builtin_convertvector(v, bf16x2_t)); }
; #define NA_STORE(sidx) do { LAS bf16* d_ = buf + ((sidx) & 1) * 9216; _Pragma("unroll") for (int q_ = 0; q_ < 2; ++q_) *(LAS v4u*)(d_ + q_ * 4608 + lrow * 72 + lseg * 8) = ld[(sidx) & 1][q_]; } while (0)
; template <bool LOCAL>
; __device__ __forceinline__ void na_unit(const bf16* P, const bf16* VT, bf16* YCAT, const LAS float* rpb_l, LAS bf16* buf, int b, int gr, int hp, int qblk, int tid) {
;     ...
;                 const int cc = c - NLOC;
; #pragma unroll
;                 for (int p2 = 0; p2 < 2; ++p2) {
;                     float p[8];
; #pragma unroll
;                     for (int e = 0; e < 4; ++e) { p[e] = __expf(sc[4 * (cc >= 0 ? cc : 0) + 2 * p2][e] - m); p[4 + e] = __expf(sc[4 * (cc >= 0 ? cc : 0) + 2 * p2 + 1][e] - m); }
; #pragma unroll
;                     for (int e = 0; e < 8; ++e) lsum += p[e];
;                     const bf16x8 pf = __builtin_bit_cast(bf16x8, (v4u){pg8::cvt_pk_bf16(p[0], p[1]), pg8::cvt_pk_bf16(p[2], p[3]), pg8::cvt_pk_bf16(p[4], p[5]), pg8::cvt_pk_bf16(p[6], p[7])});
; #pragma unroll
;                     for (int dt = 0; dt < 4; ++dt) { const LAS bf16* vp = cb + (16 * dt + fr) * 72 + 32 * p2 + 4 * fq;
;                         o[dt] = __builtin_amdgcn_mfma_f32_16x16x32_bf16(frag44(vp, vp + 16), pf, o[dt], 0, 0, 0); }
;                 }
;             }
;         }
;         if (sidx + 1 < 2 * NCH) NA_STORE(sidx + 1);
	v_exp_f32_e32 v118, v46
	v_exp_f32_e32 v123, v42
	v_fma_f32 v42, v49, s71, -v77
	ds_read2_b64 v[46:49], v124 offset1:4
	v_mul_f32_e32 v42, 0x3fb8aa3b, v42
	v_exp_f32_e32 v125, v42
	v_fma_f32 v42, v45, s71, -v77
	v_mul_f32_e32 v42, 0x3fb8aa3b, v42
	v_exp_f32_e32 v134, v42
	v_cvt_pk_bf16_f32 v42, v118, v120
	v_cvt_pk_bf16_f32 v43, v122, v125
	v_cvt_pk_bf16_f32 v44, v119, v121
	v_cvt_pk_bf16_f32 v45, v123, v134
	v_mul_f32_e32 v26, 0x3fb8aa3b, v26
	v_fma_f32 v34, v34, s71, -v77
	s_waitcnt lgkmcnt(0)
	v_mfma_f32_16x16x32_bf16 v[46:49], v[46:49], v[42:45], v[94:97]
	v_mul_f32_e32 v34, 0x3fb8aa3b, v34
	v_fma_f32 v30, v30, s71, -v77
	v_mul_f32_e32 v30, 0x3fb8aa3b, v30
	ds_read2_b64 v[94:97], v135 offset0:32 offset1:36
	s_waitcnt lgkmcnt(0)
	v_mfma_f32_16x16x32_bf16 v[94:97], v[94:97], v[42:45], v[110:113]
	s_nop 2
	v_add_u32_e32 v110, 0x5800, v68
	v_add_u32_e32 v111, 0x6000, v68
	ds_read2_b64 v[98:101], v110 offset0:64 offset1:68
	ds_read2_b64 v[102:105], v111 offset0:96 offset1:100
	s_waitcnt lgkmcnt(1)
	v_mfma_f32_16x16x32_bf16 v[98:101], v[98:101], v[42:45], v[114:117]
	v_fma_f32 v38, v38, s71, -v77
	v_mul_f32_e32 v38, 0x3fb8aa3b, v38
	v_fma_f32 v18, v18, s71, -v77
	s_waitcnt lgkmcnt(0)
	v_mfma_f32_16x16x32_bf16 v[42:45], v[102:105], v[42:45], v[106:109]
	v_mul_f32_e32 v18, 0x3fb8aa3b, v18
	v_fma_f32 v10, v10, s71, -v77
	v_mul_f32_e32 v10, 0x3fb8aa3b, v10
	v_exp_f32_e32 v107, v26
	v_fma_f32 v26, v35, s71, -v77
	v_mul_f32_e32 v26, 0x3fb8aa3b, v26
	v_exp_f32_e32 v108, v26
	v_fma_f32 v26, v27, s71, -v77
	v_mul_f32_e32 v26, 0x3fb8aa3b, v26
	v_exp_f32_e32 v109, v26
	v_fma_f32 v26, v36, s71, -v77
	v_mul_f32_e32 v26, 0x3fb8aa3b, v26
	v_exp_f32_e32 v112, v26
	v_fma_f32 v26, v28, s71, -v77
	v_mul_f32_e32 v26, 0x3fb8aa3b, v26
	v_exp_f32_e32 v106, v34
	v_exp_f32_e32 v113, v26
	v_fma_f32 v26, v37, s71, -v77
	ds_read2_b64 v[34:37], v124 offset0:8 offset1:12
	v_mul_f32_e32 v26, 0x3fb8aa3b, v26
	v_exp_f32_e32 v114, v26
	v_fma_f32 v26, v29, s71, -v77
	v_mul_f32_e32 v26, 0x3fb8aa3b, v26
	v_exp_f32_e32 v115, v26
	v_cvt_pk_bf16_f32 v26, v106, v108
	v_cvt_pk_bf16_f32 v27, v112, v114
	v_cvt_pk_bf16_f32 v28, v107, v109
	v_cvt_pk_bf16_f32 v29, v113, v115
	v_fma_f32 v2, v2, s71, -v77
	v_mul_f32_e32 v2, 0x3fb8aa3b, v2
	s_waitcnt lgkmcnt(0)
	v_mfma_f32_16x16x32_bf16 v[34:37], v[34:37], v[26:29], v[46:49]
	v_fma_f32 v6, v6, s71, -v77
	v_mul_f32_e32 v6, 0x3fb8aa3b, v6
	s_nop 0
	ds_read2_b64 v[46:49], v135 offset0:40 offset1:44
	s_waitcnt lgkmcnt(0)
	v_mfma_f32_16x16x32_bf16 v[46:49], v[46:49], v[26:29], v[94:97]
	s_nop 2
	ds_read2_b64 v[94:97], v110 offset0:72 offset1:76
	s_waitcnt lgkmcnt(0)
	v_mfma_f32_16x16x32_bf16 v[94:97], v[94:97], v[26:29], v[98:101]
	s_nop 2
	ds_read2_b64 v[98:101], v111 offset0:104 offset1:108
	global_load_dwordx4 v[102:105], v[78:79], off offset:384
	s_nop 0
	global_load_dwordx4 v[78:81], v[80:81], off offset:384
	s_waitcnt vmcnt(5)
	ds_write_b128 v73, v[126:129]
	s_waitcnt vmcnt(4)
	ds_write_b128 v73, v[130:133] offset:9216
	s_waitcnt lgkmcnt(2)
	v_mfma_f32_16x16x32_bf16 v[26:29], v[98:101], v[26:29], v[42:45]
	v_exp_f32_e32 v99, v30
	v_fma_f32 v30, v39, s71, -v77
	v_mul_f32_e32 v30, 0x3fb8aa3b, v30
	v_exp_f32_e32 v100, v30
	v_fma_f32 v30, v31, s71, -v77
	v_mul_f32_e32 v30, 0x3fb8aa3b, v30
	v_exp_f32_e32 v101, v30
	v_fma_f32 v30, v40, s71, -v77
	v_mul_f32_e32 v30, 0x3fb8aa3b, v30
	v_exp_f32_e32 v116, v30
	v_fma_f32 v30, v32, s71, -v77
	v_mul_f32_e32 v30, 0x3fb8aa3b, v30
	s_waitcnt lgkmcnt(0)
	s_barrier
	v_exp_f32_e32 v98, v38
	v_exp_f32_e32 v117, v30
	v_fma_f32 v30, v41, s71, -v77
	ds_read2_b64 v[38:41], v68 offset1:4
	v_mul_f32_e32 v30, 0x3fb8aa3b, v30
	v_exp_f32_e32 v126, v30
	v_fma_f32 v30, v33, s71, -v77
	v_mul_f32_e32 v30, 0x3fb8aa3b, v30
	v_exp_f32_e32 v127, v30
	v_cvt_pk_bf16_f32 v30, v98, v100
	v_cvt_pk_bf16_f32 v31, v116, v126
	v_cvt_pk_bf16_f32 v32, v99, v101
	v_cvt_pk_bf16_f32 v33, v117, v127
	ds_read2_b64 v[42:45], v89 offset0:64 offset1:68
	s_waitcnt lgkmcnt(1)
	v_mfma_f32_16x16x32_bf16 v[34:37], v[38:41], v[30:33], v[34:37]
	ds_read2_b64 v[38:41], v69 offset0:32 offset1:36
	s_waitcnt lgkmcnt(0)
	v_mfma_f32_16x16x32_bf16 v[38:41], v[38:41], v[30:33], v[46:49]
	s_nop 2
	ds_read2_b64 v[46:49], v93 offset0:96 offset1:100
	s_waitcnt lgkmcnt(0)
	v_mfma_f32_16x16x32_bf16 v[26:29], v[46:49], v[30:33], v[26:29]
	v_exp_f32_e32 v46, v18
	v_fma_f32 v18, v22, s71, -v77
	v_mul_f32_e32 v18, 0x3fb8aa3b, v18
	v_exp_f32_e32 v47, v18
	v_fma_f32 v18, v19, s71, -v77
	v_mul_f32_e32 v18, 0x3fb8aa3b, v18
	v_exp_f32_e32 v48, v18
	v_fma_f32 v18, v23, s71, -v77
	v_mul_f32_e32 v18, 0x3fb8aa3b, v18
	v_exp_f32_e32 v49, v18
	v_fma_f32 v18, v20, s71, -v77
	v_mul_f32_e32 v18, 0x3fb8aa3b, v18
	v_mfma_f32_16x16x32_bf16 v[42:45], v[42:45], v[30:33], v[94:97]
	ds_read2_b64 v[30:33], v69 offset0:40 offset1:44
	s_nop 1
	v_exp_f32_e32 v94, v18
	v_fma_f32 v18, v24, s71, -v77
	v_mul_f32_e32 v18, 0x3fb8aa3b, v18
	v_exp_f32_e32 v95, v18
	v_fma_f32 v18, v21, s71, -v77
	v_mul_f32_e32 v22, 0x3fb8aa3b, v18
	ds_read2_b64 v[18:21], v68 offset0:8 offset1:12
	v_exp_f32_e32 v68, v22
	v_fma_f32 v22, v25, s71, -v77
	v_mul_f32_e32 v22, 0x3fb8aa3b, v22
	v_exp_f32_e32 v96, v22
	v_cvt_pk_bf16_f32 v22, v46, v48
	v_cvt_pk_bf16_f32 v23, v94, v68
	v_cvt_pk_bf16_f32 v24, v47, v49
	v_cvt_pk_bf16_f32 v25, v95, v96
	s_waitcnt lgkmcnt(0)
	s_nop 0
	v_mfma_f32_16x16x32_bf16 v[18:21], v[18:21], v[22:25], v[34:37]
	v_mfma_f32_16x16x32_bf16 v[30:33], v[30:33], v[22:25], v[38:41]
	s_nop 1
	ds_read2_b64 v[34:37], v89 offset0:72 offset1:76
	ds_read2_b64 v[38:41], v93 offset0:104 offset1:108
	s_waitcnt lgkmcnt(1)
	v_mfma_f32_16x16x32_bf16 v[34:37], v[34:37], v[22:25], v[42:45]
	s_waitcnt vmcnt(1)
	ds_write_b128 v73, v[102:105] offset:18432
	s_waitcnt vmcnt(0)
	ds_write_b128 v73, v[78:81] offset:27648
	s_waitcnt lgkmcnt(0)
	s_barrier
; #define LAS __attribute__((address_space(3)))
; __device__ __forceinline__ unsigned cvt_pk_bf16(float lo, float hi) { const float __attribute__((ext_vector_type(2))) v = {lo, hi}; return __builtin_bit_cast(unsigned, __builtin_convertvector(v, bf16x2_t)); }
; #define NA_STORE(sidx) do { LAS bf16* d_ = buf + ((sidx) & 1) * 9216; _Pragma("unroll") for (int q_ = 0; q_ < 2; ++q_) *(LAS v4u*)(d_ + q_ * 4608 + lrow * 72 + lseg * 8) = ld[(sidx) & 1][q_]; } while (0)
; template <bool LOCAL>
; __device__ __forceinline__ void na_unit(const bf16* P, const bf16* VT, bf16* YCAT, const LAS float* rpb_l, LAS bf16* buf, int b, int gr, int hp, int qblk, int tid) {
;     ...
;                 const int cc = c - NLOC;
; #pragma unroll
;                 for (int p2 = 0; p2 < 2; ++p2) {
;                     float p[8];
; #pragma unroll
;                     for (int e = 0; e < 4; ++e) { p[e] = __expf(sc[4 * (cc >= 0 ? cc : 0) + 2 * p2][e] - m); p[4 + e] = __expf(sc[4 * (cc >= 0 ? cc : 0) + 2 * p2 + 1][e] - m); }
; #pragma unroll
;                     for (int e = 0; e < 8; ++e) lsum += p[e];
;                     const bf16x8 pf = __builtin_bit_cast(bf16x8, (v4u){pg8::cvt_pk_bf16(p[0], p[1]), pg8::cvt_pk_bf16(p[2], p[3]), pg8::cvt_pk_bf16(p[4], p[5]), pg8::cvt_pk_bf16(p[6], p[7])});
; #pragma unroll
;                     for (int dt = 0; dt < 4; ++dt) { const LAS bf16* vp = cb + (16 * dt + fr) * 72 + 32 * p2 + 4 * fq;
;                         o[dt] = __builtin_amdgcn_mfma_f32_16x16x32_bf16(frag44(vp, vp + 16), pf, o[dt], 0, 0, 0); }
;                 }
;             }
;         }
;         if (sidx + 1 < 2 * NCH) NA_STORE(sidx + 1);
;         __syncthreads();
;     }
;     ...
;     lsum += __shfl_xor(lsum, 16); lsum += __shfl_xor(lsum, 32);
;     const float inv = 1.f / lsum;
;     bf16* op = YCAT + (size_t)(qrow0 + fr) * D + 512 + h * 64 + 4 * fq;
; #pragma unroll
;     for (int dt = 0; dt < 4; ++dt) { v2u w; w.x = pg8::cvt_pk_bf16(o[dt][0] * inv, o[dt][1] * inv); w.y = pg8::cvt_pk_bf16(o[dt][2] * inv, o[dt][3] * inv); *(v2u*)(op + dt * 16) = w; }
	v_mfma_f32_16x16x32_bf16 v[22:25], v[38:41], v[22:25], v[26:29]
	v_exp_f32_e32 v38, v10
	v_fma_f32 v10, v14, s71, -v77
	v_mul_f32_e32 v10, 0x3fb8aa3b, v10
	v_exp_f32_e32 v39, v10
	v_fma_f32 v10, v11, s71, -v77
	v_mul_f32_e32 v10, 0x3fb8aa3b, v10
	v_exp_f32_e32 v40, v10
	v_fma_f32 v10, v15, s71, -v77
	v_mul_f32_e32 v10, 0x3fb8aa3b, v10
	v_exp_f32_e32 v41, v10
	v_fma_f32 v10, v12, s71, -v77
	v_mul_f32_e32 v10, 0x3fb8aa3b, v10
	v_exp_f32_e32 v42, v10
	v_fma_f32 v10, v16, s71, -v77
	v_mul_f32_e32 v10, 0x3fb8aa3b, v10
	v_exp_f32_e32 v43, v10
	v_fma_f32 v10, v13, s71, -v77
	ds_read2_b64 v[26:29], v110 offset0:64 offset1:68
	v_mul_f32_e32 v14, 0x3fb8aa3b, v10
	v_exp_f32_e32 v44, v14
	v_fma_f32 v14, v17, s71, -v77
	v_mul_f32_e32 v14, 0x3fb8aa3b, v14
	v_exp_f32_e32 v45, v14
	v_cvt_pk_bf16_f32 v14, v38, v40
	v_cvt_pk_bf16_f32 v15, v42, v44
	v_cvt_pk_bf16_f32 v16, v39, v41
	v_cvt_pk_bf16_f32 v17, v43, v45
	ds_read2_b64 v[10:13], v124 offset1:4
	v_mov_b32_e32 v73, v71
	s_waitcnt lgkmcnt(1)
	v_mfma_f32_16x16x32_bf16 v[26:29], v[26:29], v[14:17], v[34:37]
	s_nop 2
	v_add_f32_e32 v34, 0, v53
	v_add_f32_e32 v34, v63, v34
	v_add_f32_e32 v34, v66, v34
	v_add_f32_e32 v34, v67, v34
	v_add_f32_e32 v34, v52, v34
	v_add_f32_e32 v34, v62, v34
	v_add_f32_e32 v34, v64, v34
	v_add_f32_e32 v34, v65, v34
	v_add_f32_e32 v34, v58, v34
	v_add_f32_e32 v34, v59, v34
	v_add_f32_e32 v34, v60, v34
	v_add_f32_e32 v34, v61, v34
	v_add_f32_e32 v34, v54, v34
	v_add_f32_e32 v34, v55, v34
	v_add_f32_e32 v34, v56, v34
	v_add_f32_e32 v34, v57, v34
	s_waitcnt lgkmcnt(0)
	v_mfma_f32_16x16x32_bf16 v[10:13], v[10:13], v[14:17], v[18:21]
	v_add_f32_e32 v34, v118, v34
	v_add_f32_e32 v34, v120, v34
	v_add_f32_e32 v34, v122, v34
	ds_read2_b64 v[18:21], v135 offset0:32 offset1:36
	v_add_f32_e32 v34, v125, v34
	v_add_f32_e32 v34, v119, v34
	v_add_f32_e32 v34, v121, v34
	v_add_f32_e32 v34, v123, v34
	v_add_f32_e32 v34, v134, v34
	v_add_f32_e32 v34, v106, v34
	s_waitcnt lgkmcnt(0)
	v_mfma_f32_16x16x32_bf16 v[18:21], v[18:21], v[14:17], v[30:33]
	v_add_f32_e32 v34, v108, v34
	s_nop 1
	ds_read2_b64 v[30:33], v111 offset0:96 offset1:100
	v_add_f32_e32 v34, v112, v34
	v_add_f32_e32 v34, v114, v34
	v_add_f32_e32 v34, v107, v34
	v_add_f32_e32 v34, v109, v34
	v_add_f32_e32 v34, v113, v34
	v_add_f32_e32 v34, v115, v34
	v_add_f32_e32 v34, v98, v34
	v_add_f32_e32 v34, v100, v34
	s_waitcnt lgkmcnt(0)
	v_mfma_f32_16x16x32_bf16 v[14:17], v[30:33], v[14:17], v[22:25]
	v_add_f32_e32 v34, v116, v34
	v_add_f32_e32 v34, v126, v34
	v_add_f32_e32 v34, v99, v34
	v_exp_f32_e32 v23, v2
	v_fma_f32 v2, v7, s71, -v77
	v_mul_f32_e32 v2, 0x3fb8aa3b, v2
	v_exp_f32_e32 v24, v2
	v_fma_f32 v2, v3, s71, -v77
	v_mul_f32_e32 v2, 0x3fb8aa3b, v2
	v_add_f32_e32 v34, v101, v34
	v_exp_f32_e32 v25, v2
	v_fma_f32 v2, v8, s71, -v77
	v_add_f32_e32 v34, v117, v34
	v_mul_f32_e32 v2, 0x3fb8aa3b, v2
	v_add_f32_e32 v34, v127, v34
	v_exp_f32_e32 v30, v2
	v_fma_f32 v2, v4, s71, -v77
	v_add_f32_e32 v34, v46, v34
	v_mul_f32_e32 v2, 0x3fb8aa3b, v2
	v_add_f32_e32 v34, v48, v34
	v_exp_f32_e32 v22, v6
	v_exp_f32_e32 v31, v2
	v_fma_f32 v2, v9, s71, -v77
	ds_read2_b64 v[6:9], v124 offset0:8 offset1:12
	v_add_f32_e32 v34, v94, v34
	v_mul_f32_e32 v2, 0x3fb8aa3b, v2
	v_add_f32_e32 v34, v68, v34
	v_exp_f32_e32 v32, v2
	v_fma_f32 v2, v5, s71, -v77
	v_add_f32_e32 v34, v47, v34
	v_mul_f32_e32 v2, 0x3fb8aa3b, v2
	v_add_f32_e32 v34, v49, v34
	v_exp_f32_e32 v33, v2
	v_add_f32_e32 v34, v95, v34
	v_add_f32_e32 v34, v96, v34
	v_add_f32_e32 v34, v38, v34
	v_add_f32_e32 v34, v40, v34
	v_cvt_pk_bf16_f32 v2, v22, v24
	v_cvt_pk_bf16_f32 v3, v30, v32
	v_cvt_pk_bf16_f32 v4, v23, v25
	v_cvt_pk_bf16_f32 v5, v31, v33
	v_add_f32_e32 v34, v42, v34
	v_add_f32_e32 v34, v44, v34
	s_waitcnt lgkmcnt(0)
	v_mfma_f32_16x16x32_bf16 v[6:9], v[6:9], v[2:5], v[10:13]
	v_add_f32_e32 v34, v39, v34
	v_add_f32_e32 v34, v41, v34
	v_add_f32_e32 v34, v43, v34
	ds_read2_b64 v[10:13], v135 offset0:40 offset1:44
	v_add_f32_e32 v34, v45, v34
	v_add_f32_e32 v22, v22, v34
	v_add_f32_e32 v22, v24, v22
	v_add_f32_e32 v22, v30, v22
	v_add_f32_e32 v22, v32, v22
	s_waitcnt lgkmcnt(0)
	v_mfma_f32_16x16x32_bf16 v[10:13], v[10:13], v[2:5], v[18:21]
	s_nop 2
	ds_read2_b64 v[18:21], v110 offset0:72 offset1:76
	v_add_f32_e32 v22, v23, v22
	v_add_f32_e32 v22, v25, v22
	v_add_f32_e32 v22, v31, v22
	v_add_f32_e32 v30, v33, v22
	ds_bpermute_b32 v31, v50, v30
	ds_read2_b64 v[22:25], v111 offset0:104 offset1:108
	s_waitcnt lgkmcnt(2)
	v_mfma_f32_16x16x32_bf16 v[18:21], v[18:21], v[2:5], v[26:29]
	v_mov_b32_e32 v77, v71
	s_waitcnt lgkmcnt(1)
	s_nop 0
	v_add_f32_e32 v26, v30, v31
	ds_bpermute_b32 v27, v51, v26
	s_waitcnt lgkmcnt(1)
	v_mfma_f32_16x16x32_bf16 v[14:17], v[22:25], v[2:5], v[14:17]
	s_waitcnt lgkmcnt(0)
	v_add_f32_e32 v2, v26, v27
	v_div_scale_f32 v3, s[0:1], v2, v2, 1.0
	v_rcp_f32_e32 v4, v3
	s_barrier
	s_mov_b64 s[0:1], 0
	v_fma_f32 v5, -v3, v4, 1.0
	v_fmac_f32_e32 v4, v5, v4
	v_div_scale_f32 v5, vcc, 1.0, v2, 1.0
	v_mul_f32_e32 v22, v5, v4
	v_fma_f32 v23, -v3, v22, v5
	v_fmac_f32_e32 v22, v23, v4
	v_fma_f32 v3, -v3, v22, v5
	v_div_fmas_f32 v3, v3, v4, v22
	v_div_fixup_f32 v22, v3, v2, 1.0
	v_lshlrev_b64 v[2:3], 11, v[72:73]
	v_lshl_add_u64 v[2:3], s[10:11], 0, v[2:3]
	v_lshl_add_u64 v[2:3], v[2:3], 0, v[74:75]
	v_pk_mul_f32 v[6:7], v[6:7], v[22:23] op_sel_hi:[1,0]
	v_pk_mul_f32 v[8:9], v[8:9], v[22:23] op_sel_hi:[1,0]
	v_lshl_add_u64 v[4:5], v[2:3], 0, v[76:77]
	v_cvt_pk_bf16_f32 v6, v6, v7
	v_cvt_pk_bf16_f32 v7, v8, v9
	global_store_dwordx2 v[4:5], v[6:7], off offset:1024
	v_pk_mul_f32 v[6:7], v[10:11], v[22:23] op_sel_hi:[1,0]
	v_pk_mul_f32 v[8:9], v[12:13], v[22:23] op_sel_hi:[1,0]
	v_cvt_pk_bf16_f32 v6, v6, v7
	v_cvt_pk_bf16_f32 v7, v8, v9
	global_store_dwordx2 v[4:5], v[6:7], off offset:1056
	v_pk_mul_f32 v[6:7], v[18:19], v[22:23] op_sel_hi:[1,0]
	v_pk_mul_f32 v[8:9], v[20:21], v[22:23] op_sel_hi:[1,0]
	v_cvt_pk_bf16_f32 v6, v6, v7
	v_cvt_pk_bf16_f32 v7, v8, v9
	v_lshl_add_u64 v[2:3], v[4:5], 0, s[12:13]
	global_store_dwordx2 v[4:5], v[6:7], off offset:1088
	v_pk_mul_f32 v[4:5], v[14:15], v[22:23] op_sel_hi:[1,0]
	v_pk_mul_f32 v[6:7], v[16:17], v[22:23] op_sel_hi:[1,0]
	v_cvt_pk_bf16_f32 v4, v4, v5

; #define LAS __attribute__((address_space(3)))
; template <bool LOCAL>
; __device__ __forceinline__ void na_unit(const bf16* P, const bf16* VT, bf16* YCAT, const LAS float* rpb_l, LAS bf16* buf, int b, int gr, int hp, int qblk, int tid) {
;     typedef pg8::bf16x8 bf16x8;
;     constexpr int NCH = LOCAL ? 12 : 4, NLOC = LOCAL ? 8 : 0;
;     const int lane = tid & 63, wv = tid >> 6, fr = lane & 15, fq = lane >> 4, hh = wv >> 2, qb = wv & 3, h = 2 * hp + hh;
;     const int qrow0 = LOCAL ? NCTX + b * SEQ + gr * 64 + 16 * qb : b * CTXL + qblk * 64 + 16 * qb;
;     const int r0 = min(max(gr - 4, 0), 24);
;     const int kc0 = qb == 0 ? 0 : qb == 1 ? 8 : qb == 2 ? 24 : 32;
;     const int qcol = 16 * qb + fr, cs = min(max(qcol - 8, 0), 48);
;     const LAS float* rpb = rpb_l + h * 15 * 31;
;     v4u ld[2][2];
;     const int lrow = (tid >> 3) & 63, lseg = tid & 7;
;     ...
;     bf16x8 qf[2];
; #pragma unroll
;     for (int ks = 0; ks < 2; ++ks) qf[ks] = *(const bf16x8*)(P + (size_t)(qrow0 + fr) * DINP + h * 64 + 32 * ks + 8 * fq);
;     f32x4 sl[16], sc[16];
;     float m = -1.0e30f, lsum = 0.f;
;     f32x4 o[4];
; #pragma unroll
;     for (int dt = 0; dt < 4; ++dt) o[dt] = (f32x4){0.f, 0.f, 0.f, 0.f};
;     NA_ISSUE(0); NA_ISSUE(1); NA_STORE(0);
;     __syncthreads();
; #pragma unroll
;     for (int sidx = 0; sidx < 2 * NCH; ++sidx) {
;         if (sidx + 2 < 2 * NCH) NA_ISSUE(sidx + 2);
;         const LAS bf16* cb = buf + (sidx & 1) * 9216 + hh * 4608;
;         if (sidx < NCH) {
;             const int c = sidx;
;             if (LOCAL && c < 8) {
; #pragma unroll
;                 for (int t2 = 0; t2 < 2; ++t2) {
;                     const LAS bf16* kp = cb + (kc0 + 16 * t2 + fr) * 72 + 8 * fq;
;                     f32x4 acc = {0.f, 0.f, 0.f, 0.f};
;                     acc = __builtin_amdgcn_mfma_f32_16x16x32_bf16(*(const LAS bf16x8*)(kp), qf[0], acc, 0, 0, 0);
;                     acc = __builtin_amdgcn_mfma_f32_16x16x32_bf16(*(const LAS bf16x8*)(kp + 32), qf[1], acc, 0, 0, 0);
;                     const LAS float* rb = rpb + (r0 + c - gr + 7) * 31 + 15 - qcol;
; #pragma unroll
;                     for (int e = 0; e < 4; ++e) { const int kcol = kc0 + 16 * t2 + 4 * fq + e; const bool ok = (kcol >= cs) && (kcol < cs + 16);
;                         const float sv = ok ? acc[e] * 0.125f + rb[ok ? kcol : qcol] : -1.0e30f; acc[e] = sv; m = fmaxf(m, sv); }
.LBB0_1746:
	s_or_b64 exec, exec, s[0:1]
	s_bfe_u32 s19, s75, 0x50002
	v_sub_u32_e64 v3, s19, 4 clamp
	s_ashr_i32 s17, s75, 7
	v_readfirstlane_b32 s0, v3
	s_lshl_b32 s26, s17, 11
	s_min_u32 s20, s0, 24
	s_add_i32 s14, s26, 0x1000
	s_lshl_b32 s15, s20, 6
	s_or_b32 s16, s15, s14
	v_mov_b64_e32 v[18:19], s[8:9]
	v_and_b32_e32 v32, 7, v92
	v_or_b32_e32 v3, s16, v87
	s_and_b32 s18, s75, 3
	v_mad_i64_i32 v[4:5], s[0:1], v3, s69, v[18:19]
	v_lshlrev_b32_e32 v26, 4, v32
	v_mov_b32_e32 v27, v71
	v_lshl_add_u64 v[4:5], v[4:5], 0, v[26:27]
	s_lshl_b32 s2, s18, 8
	v_lshl_add_u64 v[4:5], v[4:5], 0, s[2:3]
	global_load_dwordx4 v[10:13], v[4:5], off offset:1024
	global_load_dwordx4 v[14:17], v[4:5], off offset:1152
	s_lshl_b32 s0, s19, 6
	v_lshl_or_b32 v31, v2, 4, v88
	v_lshl_add_u32 v33, s18, 1, v91
	s_or_b32 s0, s14, s0
	v_mad_u32_u24 v2, v87, s70, 0
	v_lshlrev_b32_e32 v72, 6, v33
	s_add_i32 s50, s26, 0x1040
	v_or_b32_e32 v74, s0, v31
	v_add_u32_e32 v75, v2, v26
	v_ashrrev_i32_e32 v73, 31, v72
	v_or_b32_e32 v4, s50, v87
	v_mad_i64_i32 v[2:3], s[0:1], v74, s69, v[18:19]
	v_add_u32_e32 v4, s15, v4
	v_lshl_add_u64 v[2:3], v[72:73], 1, v[2:3]
	v_mad_i64_i32 v[4:5], s[0:1], v4, s69, v[18:19]
	v_lshl_add_u64 v[2:3], v[2:3], 0, v[70:71]
	v_lshl_add_u64 v[20:21], v[4:5], 0, v[26:27]
	global_load_dwordx4 v[6:9], v[2:3], off
	s_nop 0
	global_load_dwordx4 v[2:5], v[2:3], off offset:64
	s_or_b32 s14, s26, s15
	s_addk_i32 s14, 0x1080
	v_or_b32_e32 v24, s14, v87
	v_mad_i64_i32 v[28:29], s[0:1], v24, s69, v[18:19]
	v_lshl_add_u64 v[26:27], v[28:29], 0, v[26:27]
	v_lshl_add_u64 v[22:23], v[20:21], 0, s[2:3]
	v_lshl_add_u64 v[26:27], v[26:27], 0, s[2:3]
	s_mov_b32 s100, 0x60000
	s_mov_b32 s101, 0
	v_lshl_add_u64 v[248:249], v[22:23], 0, s[100:101]
	global_load_dwordx4 v[18:21], v[22:23], off offset:1024
	s_nop 0
	global_load_dwordx4 v[22:25], v[22:23], off offset:1152
	global_load_dword v250, v[248:249], off offset:1024
	global_load_dword v251, v[248:249], off offset:1152
	v_add_u32_e32 v30, v85, v70
	v_add_u32_e32 v34, v89, v88
	v_mad_u32_u24 v36, v34, s70, v30
	s_movk_i32 s0, 0x744
	v_mul_lo_u32 v33, v33, s0
	s_sub_i32 s0, s20, s19
	s_mulk_i32 s0, 0x7c
	v_sub_u32_e64 v35, v31, 8 clamp
	s_add_i32 s0, s0, 0
	v_min_u32_e32 v35, 48, v35
	v_lshlrev_b32_e32 v77, 2, v90
	v_add_u32_e32 v33, s0, v33
	v_lshlrev_b32_e32 v31, 2, v31
	v_sub_u32_e32 v31, v33, v31
	v_add_u32_e32 v33, v89, v77
	v_cmp_ge_u32_e32 vcc, v33, v35
	v_mov_b32_e32 v90, 0xf149f2ca
	v_lshl_add_u32 v31, v33, 2, v31
	v_mov_b32_e32 v91, 0xf149f2ca
	s_waitcnt vmcnt(7)
	ds_write_b128 v75, v[10:13]
	s_waitcnt vmcnt(6)
	ds_write_b128 v75, v[14:17] offset:9216
	s_waitcnt lgkmcnt(0)
	s_barrier
	ds_read_b32 v240, v31 offset:37792
	ds_read_b32 v241, v31 offset:37796
	ds_read_b32 v242, v31 offset:37800
	ds_read_b32 v243, v31 offset:37804
	ds_read_b32 v244, v31 offset:37856
	ds_read_b32 v245, v31 offset:37860
	ds_read_b32 v246, v31 offset:37864
	ds_read_b32 v247, v31 offset:37868
	v_lshl_add_u64 v[248:249], v[26:27], 0, s[100:101]
	global_load_dwordx4 v[10:13], v[26:27], off offset:1024
	global_load_dwordx4 v[14:17], v[26:27], off offset:1152
	global_load_dword v250, v[248:249], off offset:1024
	global_load_dword v251, v[248:249], off offset:1152
	ds_read_b128 v[26:29], v36
	ds_read_b128 v[38:41], v36 offset:64
	s_waitcnt vmcnt(9) lgkmcnt(1)
	v_mfma_f32_16x16x32_bf16 v[26:29], v[26:29], v[6:9], 0
	v_add_u32_e32 v36, 16, v35
	v_cmp_lt_u32_e64 s[0:1], v33, v36
	s_and_b64 s[28:29], vcc, s[0:1]
	s_waitcnt vmcnt(8) lgkmcnt(0)
	v_mfma_f32_16x16x32_bf16 v[26:29], v[38:41], v[2:5], v[26:29]
	s_nop 2
	s_waitcnt lgkmcnt(0)
	s_nop 3
	v_fmac_f32_e32 v240, 0x3e000000, v26
	v_cndmask_b32_e64 v91, v91, v240, s[28:29]
	s_nop 4
	v_or_b32_e32 v26, 1, v33
	v_cmp_ge_u32_e32 vcc, v26, v35
	v_cmp_lt_u32_e64 s[0:1], v26, v36
	s_and_b64 s[30:31], vcc, s[0:1]
	s_nop 2
	s_waitcnt lgkmcnt(0)
	v_fmac_f32_e32 v241, 0x3e000000, v27
	v_cndmask_b32_e64 v90, v90, v241, s[30:31]
	v_or_b32_e32 v26, 2, v33
	v_cmp_ge_u32_e32 vcc, v26, v35
	v_cmp_lt_u32_e64 s[0:1], v26, v36
	s_and_b64 s[34:35], vcc, s[0:1]
	v_mov_b32_e32 v92, 0xf149f2ca
	v_mov_b32_e32 v93, 0xf149f2ca
	s_nop 2
	s_waitcnt lgkmcnt(0)
	v_fmac_f32_e32 v242, 0x3e000000, v28
	v_cndmask_b32_e64 v93, v93, v242, s[34:35]
	v_or_b32_e32 v26, 3, v33
	v_cmp_ge_u32_e32 vcc, v26, v35
	v_cmp_lt_u32_e64 s[0:1], v26, v36
	s_and_b64 s[36:37], vcc, s[0:1]
	s_nop 2
	s_waitcnt lgkmcnt(0)
	v_fmac_f32_e32 v243, 0x3e000000, v29
	v_cndmask_b32_e64 v92, v92, v243, s[36:37]
	v_add_u32_e32 v37, 16, v89
	v_add_u32_e32 v33, v37, v88
	v_mad_u32_u24 v38, v33, s70, v30
	ds_read_b128 v[26:29], v38
	ds_read_b128 v[38:41], v38 offset:64
	v_add_u32_e32 v37, v37, v77
	v_cmp_ge_u32_e32 vcc, v37, v35
	v_cmp_lt_u32_e64 s[0:1], v37, v36
	s_waitcnt lgkmcnt(1)
	v_mfma_f32_16x16x32_bf16 v[26:29], v[26:29], v[6:9], 0
	s_and_b64 s[38:39], vcc, s[0:1]
	v_mov_b32_e32 v94, 0xf149f2ca
	v_mov_b32_e32 v95, 0xf149f2ca
	s_waitcnt lgkmcnt(0)
	v_mfma_f32_16x16x32_bf16 v[26:29], v[38:41], v[2:5], v[26:29]
	s_nop 2
	s_waitcnt lgkmcnt(0)
	s_nop 3
	v_fmac_f32_e32 v244, 0x3e000000, v26
	v_cndmask_b32_e64 v95, v95, v244, s[38:39]
	s_nop 4
	v_or_b32_e32 v26, 1, v37
	v_cmp_ge_u32_e32 vcc, v26, v35
	v_cmp_lt_u32_e64 s[0:1], v26, v36
	s_and_b64 s[44:45], vcc, s[0:1]
	s_nop 2
	s_waitcnt lgkmcnt(0)
	v_fmac_f32_e32 v245, 0x3e000000, v27
	v_cndmask_b32_e64 v94, v94, v245, s[44:45]
	v_or_b32_e32 v26, 2, v37
	v_cmp_ge_u32_e32 vcc, v26, v35
	v_cmp_lt_u32_e64 s[0:1], v26, v36
	s_and_b64 s[46:47], vcc, s[0:1]
	v_mov_b32_e32 v96, 0xf149f2ca
	v_mov_b32_e32 v98, 0xf149f2ca
	s_nop 2
	s_waitcnt lgkmcnt(0)
	v_fmac_f32_e32 v246, 0x3e000000, v28
	v_cndmask_b32_e64 v98, v98, v246, s[46:47]
	v_or_b32_e32 v26, 3, v37
	v_cmp_ge_u32_e32 vcc, v26, v35
	v_cmp_lt_u32_e64 s[0:1], v26, v36
	s_and_b64 s[48:49], vcc, s[0:1]
	s_nop 2
	s_waitcnt lgkmcnt(0)
	v_fmac_f32_e32 v247, 0x3e000000, v29
	v_cndmask_b32_e64 v96, v96, v247, s[48:49]
	v_mul_u32_u24_e32 v27, 0x90, v34
	v_lshlrev_b32_e32 v26, 3, v32
	v_add_u32_e32 v32, v30, v27
	s_waitcnt vmcnt(7)
	ds_write_b128 v75, v[18:21] offset:18432
	s_waitcnt vmcnt(6)
	ds_write_b128 v75, v[22:25] offset:27648
	s_waitcnt lgkmcnt(0)
	s_barrier
; #define LAS __attribute__((address_space(3)))
; template <bool LOCAL>
; __device__ __forceinline__ void na_unit(const bf16* P, const bf16* VT, bf16* YCAT, const LAS float* rpb_l, LAS bf16* buf, int b, int gr, int hp, int qblk, int tid) {
;     ...
;     for (int sidx = 0; sidx < 2 * NCH; ++sidx) {
;         if (sidx + 2 < 2 * NCH) NA_ISSUE(sidx + 2);
;         const LAS bf16* cb = buf + (sidx & 1) * 9216 + hh * 4608;
;         if (sidx < NCH) {
;             const int c = sidx;
;             if (LOCAL && c < 8) {
; #pragma unroll
;                 for (int t2 = 0; t2 < 2; ++t2) {
;                     const LAS bf16* kp = cb + (kc0 + 16 * t2 + fr) * 72 + 8 * fq;
;                     f32x4 acc = {0.f, 0.f, 0.f, 0.f};
;                     acc = __builtin_amdgcn_mfma_f32_16x16x32_bf16(*(const LAS bf16x8*)(kp), qf[0], acc, 0, 0, 0);
;                     acc = __builtin_amdgcn_mfma_f32_16x16x32_bf16(*(const LAS bf16x8*)(kp + 32), qf[1], acc, 0, 0, 0);
;                     const LAS float* rb = rpb + (r0 + c - gr + 7) * 31 + 15 - qcol;
; #pragma unroll
;                     for (int e = 0; e < 4; ++e) { const int kcol = kc0 + 16 * t2 + 4 * fq + e; const bool ok = (kcol >= cs) && (kcol < cs + 16);
;                         const float sv = ok ? acc[e] * 0.125f + rb[ok ? kcol : qcol] : -1.0e30f; acc[e] = sv; m = fmaxf(m, sv); }
;                     sl[2 * (c < 8 ? c : 0) + t2] = acc; }
	ds_read_b32 v240, v31 offset:37916
	ds_read_b32 v241, v31 offset:37920
	ds_read_b32 v242, v31 offset:37924
	ds_read_b32 v243, v31 offset:37928
	ds_read_b32 v244, v31 offset:37980
	ds_read_b32 v245, v31 offset:37984
	ds_read_b32 v246, v31 offset:37988
	ds_read_b32 v247, v31 offset:37992
	ds_read_b128 v[18:21], v32 offset:18432
	s_add_i32 s26, s26, s15
	s_add_i32 s0, s26, 0x10c0
	v_or_b32_e32 v24, s0, v87
	v_mov_b64_e32 v[22:23], s[8:9]
	s_lshl_b32 s1, s18, 7
	v_mad_i64_i32 v[22:23], s[18:19], v24, s69, v[22:23]
	v_lshlrev_b32_e32 v70, 1, v26
	v_lshl_add_u64 v[22:23], v[22:23], 0, v[70:71]
	s_lshl_b32 s2, s1, 1
	v_lshl_add_u64 v[22:23], v[22:23], 0, s[2:3]
	ds_read_b128 v[26:29], v32 offset:18496
	s_waitcnt lgkmcnt(1)
	v_mfma_f32_16x16x32_bf16 v[34:37], v[18:21], v[6:9], 0
	v_lshl_add_u64 v[248:249], v[22:23], 0, s[100:101]
	global_load_dwordx4 v[18:21], v[22:23], off offset:1024
	s_nop 0
	global_load_dwordx4 v[22:25], v[22:23], off offset:1152
	global_load_dword v250, v[248:249], off offset:1024
	global_load_dword v251, v[248:249], off offset:1152
	v_mov_b32_e32 v97, 0xf149f2ca
	v_mov_b32_e32 v99, 0xf149f2ca
	s_waitcnt lgkmcnt(0)
	v_mfma_f32_16x16x32_bf16 v[26:29], v[26:29], v[2:5], v[34:37]
	s_nop 2
	s_waitcnt lgkmcnt(0)
	s_nop 3
	v_fmac_f32_e32 v240, 0x3e000000, v26
	v_cndmask_b32_e64 v99, v99, v240, s[28:29]
	s_nop 2
	s_waitcnt lgkmcnt(0)
	s_nop 0
	v_fmac_f32_e32 v241, 0x3e000000, v27
	v_cndmask_b32_e64 v97, v97, v241, s[30:31]
	v_mov_b32_e32 v100, 0xf149f2ca
	v_mov_b32_e32 v101, 0xf149f2ca
	s_nop 2
	s_waitcnt lgkmcnt(0)
	v_fmac_f32_e32 v242, 0x3e000000, v28
	v_cndmask_b32_e64 v101, v101, v242, s[34:35]
	s_nop 2
	s_waitcnt lgkmcnt(0)
	v_fmac_f32_e32 v243, 0x3e000000, v29
	v_cndmask_b32_e64 v100, v100, v243, s[36:37]
	v_mul_u32_u24_e32 v26, 0x90, v33
	v_add_u32_e32 v33, v30, v26
	ds_read_b128 v[26:29], v33 offset:18432
	ds_read_b128 v[34:37], v33 offset:18496
	v_mov_b32_e32 v102, 0xf149f2ca
	v_mov_b32_e32 v104, 0xf149f2ca
	s_waitcnt lgkmcnt(1)
	v_mfma_f32_16x16x32_bf16 v[26:29], v[26:29], v[6:9], 0
	s_waitcnt lgkmcnt(0)
	v_mfma_f32_16x16x32_bf16 v[26:29], v[34:37], v[2:5], v[26:29]
	s_nop 2
	s_waitcnt lgkmcnt(0)
	s_nop 3
	v_fmac_f32_e32 v244, 0x3e000000, v26
	v_cndmask_b32_e64 v104, v104, v244, s[38:39]
	s_nop 2
	s_waitcnt lgkmcnt(0)
	s_nop 0
	v_fmac_f32_e32 v245, 0x3e000000, v27
	v_cndmask_b32_e64 v102, v102, v245, s[44:45]
	v_mov_b32_e32 v106, 0xf149f2ca
	v_mov_b32_e32 v108, 0xf149f2ca
	s_nop 2
	s_waitcnt lgkmcnt(0)
	v_fmac_f32_e32 v246, 0x3e000000, v28
	v_cndmask_b32_e64 v108, v108, v246, s[46:47]
	s_nop 2
	s_waitcnt lgkmcnt(0)
	v_fmac_f32_e32 v247, 0x3e000000, v29
	v_cndmask_b32_e64 v106, v106, v247, s[48:49]
	s_waitcnt vmcnt(7)
	ds_write_b128 v75, v[10:13]
	s_waitcnt vmcnt(6)
	ds_write_b128 v75, v[14:17] offset:9216
	s_waitcnt lgkmcnt(0)
	s_barrier
	ds_read_b32 v240, v31 offset:38040
	ds_read_b32 v241, v31 offset:38044
	ds_read_b32 v242, v31 offset:38048
	ds_read_b32 v243, v31 offset:38052
	ds_read_b32 v244, v31 offset:38104
	ds_read_b32 v245, v31 offset:38108
	ds_read_b32 v246, v31 offset:38112
	ds_read_b32 v247, v31 offset:38116
	ds_read_b128 v[10:13], v32
	ds_read_b128 v[26:29], v32 offset:64
	s_add_i32 s18, s26, 0x1100
	v_or_b32_e32 v16, s18, v87
	v_mov_b64_e32 v[14:15], s[8:9]
	v_mad_i64_i32 v[14:15], s[20:21], v16, s69, v[14:15]
	v_lshl_add_u64 v[14:15], v[14:15], 0, v[70:71]
	v_lshl_add_u64 v[14:15], v[14:15], 0, s[2:3]
	s_waitcnt lgkmcnt(1)
	v_mfma_f32_16x16x32_bf16 v[34:37], v[10:13], v[6:9], 0
	v_lshl_add_u64 v[248:249], v[14:15], 0, s[100:101]
	global_load_dwordx4 v[10:13], v[14:15], off offset:1024
	s_nop 0
	global_load_dwordx4 v[14:17], v[14:15], off offset:1152
	global_load_dword v250, v[248:249], off offset:1024
	global_load_dword v251, v[248:249], off offset:1152
	v_mov_b32_e32 v103, 0xf149f2ca
	v_mov_b32_e32 v105, 0xf149f2ca
	s_waitcnt lgkmcnt(0)
	v_mfma_f32_16x16x32_bf16 v[26:29], v[26:29], v[2:5], v[34:37]
	s_nop 2
	s_waitcnt lgkmcnt(0)
	s_nop 3
	v_fmac_f32_e32 v240, 0x3e000000, v26
	v_cndmask_b32_e64 v105, v105, v240, s[28:29]
	s_nop 2
	s_waitcnt lgkmcnt(0)
	s_nop 0
	v_fmac_f32_e32 v241, 0x3e000000, v27
	v_cndmask_b32_e64 v103, v103, v241, s[30:31]
	v_mov_b32_e32 v107, 0xf149f2ca
	v_mov_b32_e32 v109, 0xf149f2ca
	s_nop 2
	s_waitcnt lgkmcnt(0)
	v_fmac_f32_e32 v242, 0x3e000000, v28
	v_cndmask_b32_e64 v109, v109, v242, s[34:35]
	s_nop 2
	s_waitcnt lgkmcnt(0)
	v_fmac_f32_e32 v243, 0x3e000000, v29
	v_cndmask_b32_e64 v107, v107, v243, s[36:37]
	ds_read_b128 v[26:29], v33
	ds_read_b128 v[34:37], v33 offset:64
	v_mov_b32_e32 v110, 0xf149f2ca
	v_mov_b32_e32 v112, 0xf149f2ca
	s_waitcnt lgkmcnt(1)
	v_mfma_f32_16x16x32_bf16 v[26:29], v[26:29], v[6:9], 0
	s_waitcnt lgkmcnt(0)
	v_mfma_f32_16x16x32_bf16 v[26:29], v[34:37], v[2:5], v[26:29]
	s_nop 2
	s_waitcnt lgkmcnt(0)
	s_nop 3
	v_fmac_f32_e32 v244, 0x3e000000, v26
	v_cndmask_b32_e64 v112, v112, v244, s[38:39]
	s_nop 2
	s_waitcnt lgkmcnt(0)
	s_nop 0
	v_fmac_f32_e32 v245, 0x3e000000, v27
	v_cndmask_b32_e64 v110, v110, v245, s[44:45]
	v_mov_b32_e32 v111, 0xf149f2ca
	v_mov_b32_e32 v115, 0xf149f2ca
	s_nop 2
	s_waitcnt lgkmcnt(0)
	v_fmac_f32_e32 v246, 0x3e000000, v28
	v_cndmask_b32_e64 v115, v115, v246, s[46:47]
	s_nop 2
	s_waitcnt lgkmcnt(0)
	v_fmac_f32_e32 v247, 0x3e000000, v29
	v_cndmask_b32_e64 v111, v111, v247, s[48:49]
	s_waitcnt vmcnt(7)
	ds_write_b128 v75, v[18:21] offset:18432
	s_waitcnt vmcnt(6)
	ds_write_b128 v75, v[22:25] offset:27648
	s_waitcnt lgkmcnt(0)
	s_barrier
; #define LAS __attribute__((address_space(3)))
; template <bool LOCAL>
; __device__ __forceinline__ void na_unit(const bf16* P, const bf16* VT, bf16* YCAT, const LAS float* rpb_l, LAS bf16* buf, int b, int gr, int hp, int qblk, int tid) {
;     ...
;     for (int sidx = 0; sidx < 2 * NCH; ++sidx) {
;         if (sidx + 2 < 2 * NCH) NA_ISSUE(sidx + 2);
;         const LAS bf16* cb = buf + (sidx & 1) * 9216 + hh * 4608;
;         if (sidx < NCH) {
;             const int c = sidx;
;             if (LOCAL && c < 8) {
; #pragma unroll
;                 for (int t2 = 0; t2 < 2; ++t2) {
;                     const LAS bf16* kp = cb + (kc0 + 16 * t2 + fr) * 72 + 8 * fq;
;                     f32x4 acc = {0.f, 0.f, 0.f, 0.f};
;                     acc = __builtin_amdgcn_mfma_f32_16x16x32_bf16(*(const LAS bf16x8*)(kp), qf[0], acc, 0, 0, 0);
;                     acc = __builtin_amdgcn_mfma_f32_16x16x32_bf16(*(const LAS bf16x8*)(kp + 32), qf[1], acc, 0, 0, 0);
;                     const LAS float* rb = rpb + (r0 + c - gr + 7) * 31 + 15 - qcol;
; #pragma unroll
;                     for (int e = 0; e < 4; ++e) { const int kcol = kc0 + 16 * t2 + 4 * fq + e; const bool ok = (kcol >= cs) && (kcol < cs + 16);
;                         const float sv = ok ? acc[e] * 0.125f + rb[ok ? kcol : qcol] : -1.0e30f; acc[e] = sv; m = fmaxf(m, sv); }
;                     sl[2 * (c < 8 ? c : 0) + t2] = acc; }
	ds_read_b32 v240, v31 offset:38164
	ds_read_b32 v241, v31 offset:38168
	ds_read_b32 v242, v31 offset:38172
	ds_read_b32 v243, v31 offset:38176
	ds_read_b32 v244, v31 offset:38228
	ds_read_b32 v245, v31 offset:38232
	ds_read_b32 v246, v31 offset:38236
	ds_read_b32 v247, v31 offset:38240
	ds_read_b128 v[18:21], v32 offset:18432
	ds_read_b128 v[26:29], v32 offset:18496
	s_add_i32 s20, s26, 0x1140
	v_or_b32_e32 v24, s20, v87
	v_mov_b64_e32 v[22:23], s[8:9]
	v_mad_i64_i32 v[22:23], s[22:23], v24, s69, v[22:23]
	v_lshl_add_u64 v[22:23], v[22:23], 0, v[70:71]
	v_lshl_add_u64 v[22:23], v[22:23], 0, s[2:3]
	s_waitcnt lgkmcnt(1)
	v_mfma_f32_16x16x32_bf16 v[34:37], v[18:21], v[6:9], 0
	v_lshl_add_u64 v[248:249], v[22:23], 0, s[100:101]
	global_load_dwordx4 v[18:21], v[22:23], off offset:1024
	s_nop 0
	global_load_dwordx4 v[22:25], v[22:23], off offset:1152
	global_load_dword v250, v[248:249], off offset:1024
	global_load_dword v251, v[248:249], off offset:1152
	v_mov_b32_e32 v113, 0xf149f2ca
	v_mov_b32_e32 v114, 0xf149f2ca
	s_waitcnt lgkmcnt(0)
	v_mfma_f32_16x16x32_bf16 v[26:29], v[26:29], v[2:5], v[34:37]
	s_nop 2
	s_waitcnt lgkmcnt(0)
	s_nop 3
	v_fmac_f32_e32 v240, 0x3e000000, v26
	v_cndmask_b32_e64 v114, v114, v240, s[28:29]
	s_nop 2
	s_waitcnt lgkmcnt(0)
	s_nop 0
	v_fmac_f32_e32 v241, 0x3e000000, v27
	v_cndmask_b32_e64 v113, v113, v241, s[30:31]
	v_mov_b32_e32 v116, 0xf149f2ca
	v_mov_b32_e32 v117, 0xf149f2ca
	s_nop 2
	s_waitcnt lgkmcnt(0)
	v_fmac_f32_e32 v242, 0x3e000000, v28
	v_cndmask_b32_e64 v117, v117, v242, s[34:35]
	s_nop 2
	s_waitcnt lgkmcnt(0)
	v_fmac_f32_e32 v243, 0x3e000000, v29
	v_cndmask_b32_e64 v116, v116, v243, s[36:37]
	ds_read_b128 v[26:29], v33 offset:18432
	ds_read_b128 v[34:37], v33 offset:18496
	v_mov_b32_e32 v118, 0xf149f2ca
	v_mov_b32_e32 v120, 0xf149f2ca
	s_waitcnt lgkmcnt(1)
	v_mfma_f32_16x16x32_bf16 v[26:29], v[26:29], v[6:9], 0
	s_waitcnt lgkmcnt(0)
	v_mfma_f32_16x16x32_bf16 v[26:29], v[34:37], v[2:5], v[26:29]
	s_nop 2
	s_waitcnt lgkmcnt(0)
	s_nop 3
	v_fmac_f32_e32 v244, 0x3e000000, v26
	v_cndmask_b32_e64 v120, v120, v244, s[38:39]
	s_nop 2
	s_waitcnt lgkmcnt(0)
	s_nop 0
	v_fmac_f32_e32 v245, 0x3e000000, v27
	v_cndmask_b32_e64 v118, v118, v245, s[44:45]
	v_mov_b32_e32 v119, 0xf149f2ca
	v_mov_b32_e32 v123, 0xf149f2ca
	s_nop 2
	s_waitcnt lgkmcnt(0)
	v_fmac_f32_e32 v246, 0x3e000000, v28
	v_cndmask_b32_e64 v123, v123, v246, s[46:47]
	s_nop 2
	s_waitcnt lgkmcnt(0)
	v_fmac_f32_e32 v247, 0x3e000000, v29
	v_cndmask_b32_e64 v119, v119, v247, s[48:49]
	s_waitcnt vmcnt(7)
	ds_write_b128 v75, v[10:13]
	s_waitcnt vmcnt(6)
	ds_write_b128 v75, v[14:17] offset:9216
	s_waitcnt lgkmcnt(0)
	s_barrier
	ds_read_b32 v240, v31 offset:38288
	ds_read_b32 v241, v31 offset:38292
	ds_read_b32 v242, v31 offset:38296
	ds_read_b32 v243, v31 offset:38300
	ds_read_b32 v244, v31 offset:38352
	ds_read_b32 v245, v31 offset:38356
	ds_read_b32 v246, v31 offset:38360
	ds_read_b32 v247, v31 offset:38364
	ds_read_b128 v[10:13], v32
	ds_read_b128 v[26:29], v32 offset:64
	s_add_i32 s22, s26, 0x1180
	v_or_b32_e32 v16, s22, v87
	v_mov_b64_e32 v[14:15], s[8:9]
	v_mad_i64_i32 v[14:15], s[24:25], v16, s69, v[14:15]
	v_lshl_add_u64 v[14:15], v[14:15], 0, v[70:71]
	v_lshl_add_u64 v[14:15], v[14:15], 0, s[2:3]
	s_waitcnt lgkmcnt(1)
	v_mfma_f32_16x16x32_bf16 v[34:37], v[10:13], v[6:9], 0
	v_lshl_add_u64 v[248:249], v[14:15], 0, s[100:101]
	global_load_dwordx4 v[10:13], v[14:15], off offset:1024
	s_nop 0
	global_load_dwordx4 v[14:17], v[14:15], off offset:1152
	global_load_dword v250, v[248:249], off offset:1024
	global_load_dword v251, v[248:249], off offset:1152
	v_mov_b32_e32 v121, 0xf149f2ca
	v_mov_b32_e32 v122, 0xf149f2ca
	s_waitcnt lgkmcnt(0)
	v_mfma_f32_16x16x32_bf16 v[26:29], v[26:29], v[2:5], v[34:37]
	s_nop 2
	s_waitcnt lgkmcnt(0)
	s_nop 3
	v_fmac_f32_e32 v240, 0x3e000000, v26
	v_cndmask_b32_e64 v122, v122, v240, s[28:29]
	s_nop 2
	s_waitcnt lgkmcnt(0)
	s_nop 0
	v_fmac_f32_e32 v241, 0x3e000000, v27
	v_cndmask_b32_e64 v121, v121, v241, s[30:31]
	v_mov_b32_e32 v124, 0xf149f2ca
	v_mov_b32_e32 v125, 0xf149f2ca
	s_nop 2
	s_waitcnt lgkmcnt(0)
	v_fmac_f32_e32 v242, 0x3e000000, v28
	v_cndmask_b32_e64 v125, v125, v242, s[34:35]
	s_nop 2
	s_waitcnt lgkmcnt(0)
	v_fmac_f32_e32 v243, 0x3e000000, v29
	v_cndmask_b32_e64 v124, v124, v243, s[36:37]
	ds_read_b128 v[26:29], v33
	ds_read_b128 v[34:37], v33 offset:64
	v_mov_b32_e32 v126, 0xf149f2ca
	v_mov_b32_e32 v128, 0xf149f2ca
	s_waitcnt lgkmcnt(1)
	v_mfma_f32_16x16x32_bf16 v[26:29], v[26:29], v[6:9], 0
	s_waitcnt lgkmcnt(0)
	v_mfma_f32_16x16x32_bf16 v[26:29], v[34:37], v[2:5], v[26:29]
	s_nop 2
	s_waitcnt lgkmcnt(0)
	s_nop 3
	v_fmac_f32_e32 v244, 0x3e000000, v26
	v_cndmask_b32_e64 v128, v128, v244, s[38:39]
	s_nop 2
	s_waitcnt lgkmcnt(0)
	s_nop 0
	v_fmac_f32_e32 v245, 0x3e000000, v27
	v_cndmask_b32_e64 v126, v126, v245, s[44:45]
	v_mov_b32_e32 v127, 0xf149f2ca
	v_mov_b32_e32 v132, 0xf149f2ca
	s_nop 2
	s_waitcnt lgkmcnt(0)
	v_fmac_f32_e32 v246, 0x3e000000, v28
	v_cndmask_b32_e64 v132, v132, v246, s[46:47]
	s_nop 2
	s_waitcnt lgkmcnt(0)
	v_fmac_f32_e32 v247, 0x3e000000, v29
	v_cndmask_b32_e64 v127, v127, v247, s[48:49]
	s_waitcnt vmcnt(7)
	ds_write_b128 v75, v[18:21] offset:18432
	s_waitcnt vmcnt(6)
	ds_write_b128 v75, v[22:25] offset:27648
	s_waitcnt lgkmcnt(0)
	s_barrier
; #define LAS __attribute__((address_space(3)))
; template <bool LOCAL>
; __device__ __forceinline__ void na_unit(const bf16* P, const bf16* VT, bf16* YCAT, const LAS float* rpb_l, LAS bf16* buf, int b, int gr, int hp, int qblk, int tid) {
;     ...
;     for (int sidx = 0; sidx < 2 * NCH; ++sidx) {
;         if (sidx + 2 < 2 * NCH) NA_ISSUE(sidx + 2);
;         const LAS bf16* cb = buf + (sidx & 1) * 9216 + hh * 4608;
;         if (sidx < NCH) {
;             const int c = sidx;
;             if (LOCAL && c < 8) {
; #pragma unroll
;                 for (int t2 = 0; t2 < 2; ++t2) {
;                     const LAS bf16* kp = cb + (kc0 + 16 * t2 + fr) * 72 + 8 * fq;
;                     f32x4 acc = {0.f, 0.f, 0.f, 0.f};
;                     acc = __builtin_amdgcn_mfma_f32_16x16x32_bf16(*(const LAS bf16x8*)(kp), qf[0], acc, 0, 0, 0);
;                     acc = __builtin_amdgcn_mfma_f32_16x16x32_bf16(*(const LAS bf16x8*)(kp + 32), qf[1], acc, 0, 0, 0);
;                     const LAS float* rb = rpb + (r0 + c - gr + 7) * 31 + 15 - qcol;
; #pragma unroll
;                     for (int e = 0; e < 4; ++e) { const int kcol = kc0 + 16 * t2 + 4 * fq + e; const bool ok = (kcol >= cs) && (kcol < cs + 16);
;                         const float sv = ok ? acc[e] * 0.125f + rb[ok ? kcol : qcol] : -1.0e30f; acc[e] = sv; m = fmaxf(m, sv); }
;                     sl[2 * (c < 8 ? c : 0) + t2] = acc; }
;             } else {
;                 const int cc = c - NLOC;
	ds_read_b32 v240, v31 offset:38412
	ds_read_b32 v241, v31 offset:38416
	ds_read_b32 v242, v31 offset:38420
	ds_read_b32 v243, v31 offset:38424
	ds_read_b32 v244, v31 offset:38476
	ds_read_b32 v245, v31 offset:38480
	ds_read_b32 v246, v31 offset:38484
	ds_read_b32 v247, v31 offset:38488
	ds_read_b128 v[18:21], v32 offset:18432
	ds_read_b128 v[26:29], v32 offset:18496
	s_add_i32 s24, s26, 0x11c0
	v_or_b32_e32 v24, s24, v87
	v_mov_b64_e32 v[22:23], s[8:9]
	v_mad_i64_i32 v[22:23], s[26:27], v24, s69, v[22:23]
	v_lshl_add_u64 v[22:23], v[22:23], 0, v[70:71]
	v_lshl_add_u64 v[22:23], v[22:23], 0, s[2:3]
	s_waitcnt lgkmcnt(1)
	v_mfma_f32_16x16x32_bf16 v[34:37], v[18:21], v[6:9], 0
	global_load_dwordx4 v[18:21], v[22:23], off offset:1024
	s_nop 0
	global_load_dwordx4 v[22:25], v[22:23], off offset:1152
	v_mov_b32_e32 v129, 0xf149f2ca
	v_mov_b32_e32 v131, 0xf149f2ca
	s_waitcnt lgkmcnt(0)
	v_mfma_f32_16x16x32_bf16 v[26:29], v[26:29], v[2:5], v[34:37]
	s_nop 2
	s_waitcnt lgkmcnt(0)
	s_nop 3
	v_fmac_f32_e32 v240, 0x3e000000, v26
	v_cndmask_b32_e64 v131, v131, v240, s[28:29]
	s_nop 2
	s_waitcnt lgkmcnt(0)
	s_nop 0
	v_fmac_f32_e32 v241, 0x3e000000, v27
	v_cndmask_b32_e64 v129, v129, v241, s[30:31]
	v_mov_b32_e32 v133, 0xf149f2ca
	v_mov_b32_e32 v134, 0xf149f2ca
	s_nop 2
	s_waitcnt lgkmcnt(0)
	v_fmac_f32_e32 v242, 0x3e000000, v28
	v_cndmask_b32_e64 v134, v134, v242, s[34:35]
	s_nop 2
	s_waitcnt lgkmcnt(0)
	v_fmac_f32_e32 v243, 0x3e000000, v29
	v_cndmask_b32_e64 v133, v133, v243, s[36:37]
	ds_read_b128 v[26:29], v33 offset:18432
	ds_read_b128 v[34:37], v33 offset:18496
	v_mov_b32_e32 v136, 0xf149f2ca
	v_mov_b32_e32 v138, 0xf149f2ca
	s_waitcnt lgkmcnt(1)
	v_mfma_f32_16x16x32_bf16 v[26:29], v[26:29], v[6:9], 0
	s_waitcnt lgkmcnt(0)
	v_mfma_f32_16x16x32_bf16 v[26:29], v[34:37], v[2:5], v[26:29]
	s_nop 2
	s_waitcnt lgkmcnt(0)
	s_nop 3
	v_fmac_f32_e32 v244, 0x3e000000, v26
	v_cndmask_b32_e64 v138, v138, v244, s[38:39]
	s_nop 2
	s_waitcnt lgkmcnt(0)
	s_nop 0
	v_fmac_f32_e32 v245, 0x3e000000, v27
	v_cndmask_b32_e64 v136, v136, v245, s[44:45]
	v_mov_b32_e32 v137, 0xf149f2ca
	v_mov_b32_e32 v141, 0xf149f2ca
	s_nop 2
	s_waitcnt lgkmcnt(0)
	v_fmac_f32_e32 v246, 0x3e000000, v28
	v_cndmask_b32_e64 v141, v141, v246, s[46:47]
	s_nop 2
	s_waitcnt lgkmcnt(0)
	v_fmac_f32_e32 v247, 0x3e000000, v29
	v_cndmask_b32_e64 v137, v137, v247, s[48:49]
	s_waitcnt vmcnt(5)
	ds_write_b128 v75, v[10:13]
	s_waitcnt vmcnt(4)
	ds_write_b128 v75, v[14:17] offset:9216
	s_waitcnt lgkmcnt(0)
	s_barrier
	ds_read_b32 v240, v31 offset:38536
	ds_read_b32 v241, v31 offset:38540
	ds_read_b32 v242, v31 offset:38544
	ds_read_b32 v243, v31 offset:38548
	ds_read_b32 v244, v31 offset:38600
	ds_read_b32 v245, v31 offset:38604
	ds_read_b32 v246, v31 offset:38608
	ds_read_b32 v247, v31 offset:38612
	ds_read_b128 v[10:13], v32
	ds_read_b128 v[26:29], v32 offset:64
	s_lshl_b32 s26, s17, 8
	v_or_b32_e32 v34, s26, v87
	v_mov_b64_e32 v[14:15], s[8:9]
	v_mad_i64_i32 v[14:15], s[52:53], v34, s69, v[14:15]
	v_lshl_add_u64 v[14:15], v[14:15], 0, v[70:71]
	v_lshl_add_u64 v[14:15], v[14:15], 0, s[2:3]
	s_waitcnt lgkmcnt(1)
	v_mfma_f32_16x16x32_bf16 v[36:39], v[10:13], v[6:9], 0
	v_lshl_add_u64 v[248:249], v[14:15], 0, s[100:101]
	global_load_dwordx4 v[10:13], v[14:15], off offset:1024
	s_nop 0
	global_load_dwordx4 v[14:17], v[14:15], off offset:1152
	global_load_dword v250, v[248:249], off offset:1024
	global_load_dword v251, v[248:249], off offset:1152
	v_mov_b32_e32 v139, 0xf149f2ca
	v_mov_b32_e32 v140, 0xf149f2ca
	s_waitcnt lgkmcnt(0)
	v_mfma_f32_16x16x32_bf16 v[26:29], v[26:29], v[2:5], v[36:39]
	s_nop 2
	s_waitcnt lgkmcnt(0)
	s_nop 3
	v_fmac_f32_e32 v240, 0x3e000000, v26
	v_cndmask_b32_e64 v140, v140, v240, s[28:29]
	s_nop 2
	s_waitcnt lgkmcnt(0)
	s_nop 0
	v_fmac_f32_e32 v241, 0x3e000000, v27
	v_cndmask_b32_e64 v139, v139, v241, s[30:31]
	v_mov_b32_e32 v142, 0xf149f2ca
	v_mov_b32_e32 v143, 0xf149f2ca
	s_nop 2
	s_waitcnt lgkmcnt(0)
	v_fmac_f32_e32 v242, 0x3e000000, v28
	v_cndmask_b32_e64 v143, v143, v242, s[34:35]
	s_nop 2
	s_waitcnt lgkmcnt(0)
	v_fmac_f32_e32 v243, 0x3e000000, v29
	v_cndmask_b32_e64 v142, v142, v243, s[36:37]
	ds_read_b128 v[26:29], v33
	ds_read_b128 v[36:39], v33 offset:64
	v_mov_b32_e32 v144, 0xf149f2ca
	v_mov_b32_e32 v146, 0xf149f2ca
	s_waitcnt lgkmcnt(1)
	v_mfma_f32_16x16x32_bf16 v[26:29], v[26:29], v[6:9], 0
	s_waitcnt lgkmcnt(0)
	v_mfma_f32_16x16x32_bf16 v[26:29], v[36:39], v[2:5], v[26:29]
	s_nop 2
	s_waitcnt lgkmcnt(0)
	s_nop 3
	v_fmac_f32_e32 v244, 0x3e000000, v26
	v_cndmask_b32_e64 v146, v146, v244, s[38:39]
	s_nop 2
	s_waitcnt lgkmcnt(0)
	s_nop 0
	v_fmac_f32_e32 v245, 0x3e000000, v27
	v_cndmask_b32_e64 v144, v144, v245, s[44:45]
	v_mov_b32_e32 v145, 0xf149f2ca
	v_mov_b32_e32 v149, 0xf149f2ca
	s_nop 2
	s_waitcnt lgkmcnt(0)
	v_fmac_f32_e32 v246, 0x3e000000, v28
	v_cndmask_b32_e64 v149, v149, v246, s[46:47]
	s_nop 2
	s_waitcnt lgkmcnt(0)
	v_fmac_f32_e32 v247, 0x3e000000, v29
	v_cndmask_b32_e64 v145, v145, v247, s[48:49]
	s_waitcnt vmcnt(5)
	ds_write_b128 v75, v[18:21] offset:18432
	s_waitcnt vmcnt(4)
	ds_write_b128 v75, v[22:25] offset:27648
	s_waitcnt lgkmcnt(0)
	s_barrier
; #define LAS __attribute__((address_space(3)))
; template <bool LOCAL>
; __device__ __forceinline__ void na_unit(const bf16* P, const bf16* VT, bf16* YCAT, const LAS float* rpb_l, LAS bf16* buf, int b, int gr, int hp, int qblk, int tid) {
;     ...
;                 const int cc = c - NLOC;
; #pragma unroll
;                 for (int t4 = 0; t4 < 4; ++t4) {
;                     const LAS bf16* kp = cb + (16 * t4 + fr) * 72 + 8 * fq;
;                     f32x4 acc = {0.f, 0.f, 0.f, 0.f};
;                     acc = __builtin_amdgcn_mfma_f32_16x16x32_bf16(*(const LAS bf16x8*)(kp), qf[0], acc, 0, 0, 0);
;                     acc = __builtin_amdgcn_mfma_f32_16x16x32_bf16(*(const LAS bf16x8*)(kp + 32), qf[1], acc, 0, 0, 0);
; #pragma unroll
;                     for (int e = 0; e < 4; ++e) { acc[e] *= 0.125f; m = fmaxf(m, acc[e]); }
;                     sc[4 * (cc >= 0 ? cc : 0) + t4] = acc; }
;             }
;             if (sidx == NCH - 1) { m = fmaxf(m, __shfl_xor(m, 16)); m = fmaxf(m, __shfl_xor(m, 32)); }
	ds_read_b32 v240, v31 offset:38660
	ds_read_b32 v241, v31 offset:38664
	ds_read_b32 v242, v31 offset:38668
	ds_read_b32 v243, v31 offset:38672
	ds_read_b32 v244, v31 offset:38724
	ds_read_b32 v245, v31 offset:38728
	ds_read_b32 v246, v31 offset:38732
	ds_read_b32 v247, v31 offset:38736
	ds_read_b128 v[18:21], v32 offset:18432
	ds_read_b128 v[26:29], v32 offset:18496
	v_or_b32_e32 v24, 64, v34
	v_mov_b64_e32 v[22:23], s[8:9]
	v_mad_i64_i32 v[22:23], s[52:53], v24, s69, v[22:23]
	v_lshl_add_u64 v[22:23], v[22:23], 0, v[70:71]
	v_lshl_add_u64 v[22:23], v[22:23], 0, s[2:3]
	s_waitcnt lgkmcnt(1)
	v_mfma_f32_16x16x32_bf16 v[36:39], v[18:21], v[6:9], 0
	v_lshl_add_u64 v[248:249], v[22:23], 0, s[100:101]
	global_load_dwordx4 v[18:21], v[22:23], off offset:1024
	s_nop 0
	global_load_dwordx4 v[22:25], v[22:23], off offset:1152
	global_load_dword v250, v[248:249], off offset:1024
	global_load_dword v251, v[248:249], off offset:1152
	v_mov_b32_e32 v147, 0xf149f2ca
	v_mov_b32_e32 v148, 0xf149f2ca
	s_waitcnt lgkmcnt(0)
	v_mfma_f32_16x16x32_bf16 v[26:29], v[26:29], v[2:5], v[36:39]
	s_nop 2
	s_waitcnt lgkmcnt(0)
	s_nop 3
	v_fmac_f32_e32 v240, 0x3e000000, v26
	v_cndmask_b32_e64 v148, v148, v240, s[28:29]
	s_nop 2
	s_waitcnt lgkmcnt(0)
	s_nop 0
	v_fmac_f32_e32 v241, 0x3e000000, v27
	v_cndmask_b32_e64 v147, v147, v241, s[30:31]
	v_mov_b32_e32 v150, 0xf149f2ca
	v_mov_b32_e32 v151, 0xf149f2ca
	s_nop 2
	s_waitcnt lgkmcnt(0)
	v_fmac_f32_e32 v242, 0x3e000000, v28
	v_cndmask_b32_e64 v151, v151, v242, s[34:35]
	s_nop 2
	s_waitcnt lgkmcnt(0)
	v_fmac_f32_e32 v243, 0x3e000000, v29
	v_cndmask_b32_e64 v150, v150, v243, s[36:37]
	ds_read_b128 v[26:29], v33 offset:18432
	ds_read_b128 v[36:39], v33 offset:18496
	v_mov_b32_e32 v152, 0xf149f2ca
	v_mov_b32_e32 v154, 0xf149f2ca
	s_waitcnt lgkmcnt(1)
	v_mfma_f32_16x16x32_bf16 v[26:29], v[26:29], v[6:9], 0
	s_waitcnt lgkmcnt(0)
	v_mfma_f32_16x16x32_bf16 v[26:29], v[36:39], v[2:5], v[26:29]
	s_nop 2
	s_waitcnt lgkmcnt(0)
	s_nop 3
	v_fmac_f32_e32 v244, 0x3e000000, v26
	v_cndmask_b32_e64 v154, v154, v244, s[38:39]
	s_nop 2
	s_waitcnt lgkmcnt(0)
	s_nop 0
	v_fmac_f32_e32 v245, 0x3e000000, v27
	v_cndmask_b32_e64 v152, v152, v245, s[44:45]
	v_mov_b32_e32 v153, 0xf149f2ca
	v_mov_b32_e32 v156, 0xf149f2ca
	s_nop 2
	s_waitcnt lgkmcnt(0)
	v_fmac_f32_e32 v246, 0x3e000000, v28
	v_cndmask_b32_e64 v156, v156, v246, s[46:47]
	s_nop 2
	s_waitcnt lgkmcnt(0)
	v_fmac_f32_e32 v247, 0x3e000000, v29
	v_cndmask_b32_e64 v153, v153, v247, s[48:49]
	v_max3_f32 v26, v91, s74, v90
	v_max3_f32 v26, v26, v93, v92
	v_max3_f32 v26, v26, v95, v94
	v_max3_f32 v26, v26, v98, v96
	v_max3_f32 v26, v26, v99, v97
	v_max3_f32 v26, v26, v101, v100
	v_max3_f32 v26, v26, v104, v102
	v_max3_f32 v26, v26, v108, v106
	v_max3_f32 v26, v26, v105, v103
	v_max3_f32 v26, v26, v109, v107
	v_max3_f32 v26, v26, v112, v110
	v_max3_f32 v26, v26, v115, v111
	v_max3_f32 v26, v26, v114, v113
	v_max3_f32 v26, v26, v117, v116
	v_max3_f32 v26, v26, v120, v118
	v_max3_f32 v26, v26, v123, v119
	v_max3_f32 v26, v26, v122, v121
	v_max3_f32 v26, v26, v125, v124
	v_max3_f32 v26, v26, v128, v126
	v_max3_f32 v26, v26, v132, v127
	v_max3_f32 v26, v26, v131, v129
	v_max3_f32 v26, v26, v134, v133
	v_max3_f32 v26, v26, v138, v136
	v_max3_f32 v26, v26, v141, v137
	v_max3_f32 v26, v26, v140, v139
	v_max3_f32 v26, v26, v143, v142
	v_mad_u32_u24 v88, v88, s70, v30
	v_max3_f32 v26, v26, v146, v144
	s_waitcnt vmcnt(7)
	ds_write_b128 v75, v[10:13]
	s_waitcnt vmcnt(6)
	ds_write_b128 v75, v[14:17] offset:9216
	s_waitcnt lgkmcnt(0)
	s_barrier
	ds_read_b128 v[10:13], v88
	ds_read_b128 v[14:17], v88 offset:64
	v_max3_f32 v26, v26, v149, v145
	v_max3_f32 v26, v26, v148, v147
	v_max3_f32 v26, v26, v151, v150
	v_max3_f32 v26, v26, v154, v152
	v_max3_f32 v35, v26, v156, v153
	v_or_b32_e32 v26, 0x80, v34
	v_mov_b64_e32 v[44:45], s[8:9]
	v_mad_i64_i32 v[26:27], s[28:29], v26, s69, v[44:45]
	v_lshl_add_u64 v[26:27], v[26:27], 0, v[70:71]
	v_lshl_add_u64 v[30:31], v[26:27], 0, s[2:3]
	s_waitcnt lgkmcnt(1)
	v_mfma_f32_16x16x32_bf16 v[10:13], v[10:13], v[6:9], 0
	v_lshl_add_u64 v[248:249], v[30:31], 0, s[100:101]
	global_load_dwordx4 v[26:29], v[30:31], off offset:1024
	s_nop 0
	global_load_dwordx4 v[30:33], v[30:31], off offset:1152
	global_load_dword v250, v[248:249], off offset:1024
	global_load_dword v251, v[248:249], off offset:1152
	ds_read_b128 v[36:39], v88 offset:2304
	v_lshl_add_u64 v[78:79], s[4:5], 0, v[70:71]
	s_waitcnt lgkmcnt(1)
	v_mfma_f32_16x16x32_bf16 v[62:65], v[14:17], v[2:5], v[10:13]
	s_ashr_i32 s17, s16, 31
	v_mov_b32_e32 v81, v71
	v_cmp_lt_i32_e32 vcc, v82, v83
	ds_read_b128 v[10:13], v88 offset:2368
	v_add3_u32 v155, v85, v76, v86
	s_nop 2
	v_mul_f32_e32 v14, 0x3e000000, v62
	v_mul_f32_e32 v15, 0x3e000000, v63
	v_max3_f32 v35, v35, v14, v15
	v_mul_f32_e32 v40, 0x3e000000, v64
	s_waitcnt lgkmcnt(1)
	v_mfma_f32_16x16x32_bf16 v[14:17], v[36:39], v[6:9], 0
	v_mul_f32_e32 v36, 0x3e000000, v65
	v_max3_f32 v35, v35, v40, v36
	ds_read_b128 v[36:39], v88 offset:4608
	s_waitcnt lgkmcnt(1)
	v_mfma_f32_16x16x32_bf16 v[66:69], v[10:13], v[2:5], v[14:17]
	ds_read_b128 v[10:13], v88 offset:4672
	s_ashr_i32 s19, s18, 31
	s_ashr_i32 s21, s20, 31
	s_ashr_i32 s23, s22, 31
	s_ashr_i32 s25, s24, 31
	s_nop 2
	v_mul_f32_e32 v14, 0x3e000000, v66
	v_mul_f32_e32 v15, 0x3e000000, v67
	v_max3_f32 v35, v35, v14, v15
	s_waitcnt lgkmcnt(1)
	v_mfma_f32_16x16x32_bf16 v[14:17], v[36:39], v[6:9], 0
	v_mul_f32_e32 v40, 0x3e000000, v68
	v_mul_f32_e32 v41, 0x3e000000, v69
	v_max3_f32 v35, v35, v40, v41
	s_waitcnt lgkmcnt(0)
	v_mfma_f32_16x16x32_bf16 v[58:61], v[10:13], v[2:5], v[14:17]
	ds_read_b128 v[36:39], v88 offset:6912
	ds_read_b128 v[40:43], v88 offset:6976
	s_waitcnt vmcnt(7)
	ds_write_b128 v75, v[18:21] offset:18432
	s_waitcnt vmcnt(6)
	ds_write_b128 v75, v[22:25] offset:27648
	s_waitcnt lgkmcnt(0)
	s_nop 0
	v_mul_f32_e32 v10, 0x3e000000, v58
	v_mul_f32_e32 v11, 0x3e000000, v59
	v_max3_f32 v14, v35, v10, v11
	v_mfma_f32_16x16x32_bf16 v[10:13], v[36:39], v[6:9], 0
	v_mul_f32_e32 v15, 0x3e000000, v60
	v_mul_f32_e32 v16, 0x3e000000, v61
	v_max3_f32 v14, v14, v15, v16
	v_mfma_f32_16x16x32_bf16 v[54:57], v[40:43], v[2:5], v[10:13]
	s_barrier
; #define LAS __attribute__((address_space(3)))
; template <bool LOCAL>
; __device__ __forceinline__ void na_unit(const bf16* P, const bf16* VT, bf16* YCAT, const LAS float* rpb_l, LAS bf16* buf, int b, int gr, int hp, int qblk, int tid) {
;     ...
;                 const int cc = c - NLOC;
; #pragma unroll
;                 for (int t4 = 0; t4 < 4; ++t4) {
;                     const LAS bf16* kp = cb + (16 * t4 + fr) * 72 + 8 * fq;
;                     f32x4 acc = {0.f, 0.f, 0.f, 0.f};
;                     acc = __builtin_amdgcn_mfma_f32_16x16x32_bf16(*(const LAS bf16x8*)(kp), qf[0], acc, 0, 0, 0);
;                     acc = __builtin_amdgcn_mfma_f32_16x16x32_bf16(*(const LAS bf16x8*)(kp + 32), qf[1], acc, 0, 0, 0);
; #pragma unroll
;                     for (int e = 0; e < 4; ++e) { acc[e] *= 0.125f; m = fmaxf(m, acc[e]); }
;                     sc[4 * (cc >= 0 ? cc : 0) + t4] = acc; }
;             }
;             if (sidx == NCH - 1) { m = fmaxf(m, __shfl_xor(m, 16)); m = fmaxf(m, __shfl_xor(m, 32)); }
	v_or_b32_e32 v18, 0xc0, v34
	v_mad_i64_i32 v[18:19], s[28:29], v18, s69, v[44:45]
	v_lshl_add_u64 v[18:19], v[18:19], 0, v[70:71]
	s_nop 3
	v_mul_f32_e32 v10, 0x3e000000, v54
	v_mul_f32_e32 v11, 0x3e000000, v55
	v_max3_f32 v14, v14, v10, v11
	ds_read_b128 v[10:13], v88 offset:18432
	v_mul_f32_e32 v15, 0x3e000000, v56
	v_mul_f32_e32 v16, 0x3e000000, v57
	v_max3_f32 v35, v14, v15, v16
	ds_read_b128 v[14:17], v88 offset:18496
	v_lshl_add_u64 v[22:23], v[18:19], 0, s[2:3]
	s_waitcnt lgkmcnt(1)
	v_mfma_f32_16x16x32_bf16 v[10:13], v[10:13], v[6:9], 0
	global_load_dwordx4 v[18:21], v[22:23], off offset:1024
	global_load_dwordx4 v[158:161], v[22:23], off offset:1152
	ds_read_b128 v[22:25], v88 offset:20736
	s_ashr_i32 s27, s26, 31
	s_waitcnt lgkmcnt(1)
	v_mfma_f32_16x16x32_bf16 v[46:49], v[14:17], v[2:5], v[10:13]
	s_nop 2
	ds_read_b128 v[10:13], v88 offset:20800
	s_nop 3
	v_mul_f32_e32 v14, 0x3e000000, v46
	v_mul_f32_e32 v15, 0x3e000000, v47
	v_max3_f32 v34, v35, v14, v15
	v_mul_f32_e32 v35, 0x3e000000, v48
	s_waitcnt lgkmcnt(1)
	v_mfma_f32_16x16x32_bf16 v[14:17], v[22:25], v[6:9], 0
	v_mul_f32_e32 v22, 0x3e000000, v49
	v_max3_f32 v34, v34, v35, v22
	ds_read_b128 v[22:25], v88 offset:23040
	s_waitcnt lgkmcnt(1)
	v_mfma_f32_16x16x32_bf16 v[50:53], v[10:13], v[2:5], v[14:17]
	ds_read_b128 v[10:13], v88 offset:23104
	s_nop 6
	v_mul_f32_e32 v14, 0x3e000000, v50
	v_mul_f32_e32 v15, 0x3e000000, v51
	v_max3_f32 v34, v34, v14, v15
	s_waitcnt lgkmcnt(1)
	v_mfma_f32_16x16x32_bf16 v[14:17], v[22:25], v[6:9], 0
	v_mul_f32_e32 v35, 0x3e000000, v52
	v_mul_f32_e32 v36, 0x3e000000, v53
	v_max3_f32 v38, v34, v35, v36
	s_waitcnt lgkmcnt(0)
	v_mfma_f32_16x16x32_bf16 v[42:45], v[10:13], v[2:5], v[14:17]
	ds_read_b128 v[22:25], v88 offset:25344
	ds_read_b128 v[34:37], v88 offset:25408
	s_waitcnt vmcnt(5)
	ds_write_b128 v75, v[26:29]
	s_waitcnt vmcnt(4)
	ds_write_b128 v75, v[30:33] offset:9216
	s_waitcnt lgkmcnt(0)
	s_nop 0
	v_mul_f32_e32 v10, 0x3e000000, v42
	v_mul_f32_e32 v11, 0x3e000000, v43
	v_max3_f32 v14, v38, v10, v11
	v_mfma_f32_16x16x32_bf16 v[10:13], v[22:25], v[6:9], 0
	v_mul_f32_e32 v15, 0x3e000000, v44
	v_mul_f32_e32 v16, 0x3e000000, v45
	v_max3_f32 v14, v14, v15, v16
	v_mfma_f32_16x16x32_bf16 v[38:41], v[34:37], v[2:5], v[10:13]
	s_barrier
	v_add3_u32 v26, v87, s1, 64
	v_mul_u32_u24_e32 v26, 0x9000, v26
	v_lshl_add_u64 v[22:23], s[16:17], 1, v[78:79]
	s_nop 3
	v_mul_f32_e32 v10, 0x3e000000, v38
	v_mul_f32_e32 v11, 0x3e000000, v39
	v_max3_f32 v10, v14, v10, v11
	v_mul_f32_e32 v11, 0x3e000000, v40
	v_mul_f32_e32 v12, 0x3e000000, v41
	v_max3_f32 v34, v10, v11, v12
	v_or_b32_e32 v10, s1, v87
	v_mul_u32_u24_e32 v14, 0x9000, v10
	ds_read_b128 v[10:13], v88
	v_lshlrev_b32_e32 v70, 1, v14
	ds_read_b128 v[14:17], v88 offset:64
	v_lshlrev_b32_e32 v80, 1, v26
	v_lshl_add_u64 v[24:25], v[22:23], 0, v[70:71]
	v_lshl_add_u64 v[22:23], v[22:23], 0, v[80:81]
	s_waitcnt lgkmcnt(1)
	v_mfma_f32_16x16x32_bf16 v[10:13], v[10:13], v[6:9], 0
	v_lshl_add_u64 v[248:249], v[24:25], 0, 0
	v_lshl_add_u64 v[238:239], v[22:23], 0, 0
	global_load_dwordx4 v[162:165], v[24:25], off
	global_load_dwordx4 v[166:169], v[22:23], off
	global_load_dword v250, v[248:249], off offset:128
	global_load_dword v251, v[238:239], off offset:128
	ds_read_b128 v[22:25], v88 offset:2304
	s_add_i32 s16, s15, s50
	s_waitcnt lgkmcnt(1)
	v_mfma_f32_16x16x32_bf16 v[30:33], v[14:17], v[2:5], v[10:13]
	s_ashr_i32 s17, s16, 31
	s_ashr_i32 s15, s14, 31
	s_ashr_i32 s1, s0, 31
	ds_read_b128 v[10:13], v88 offset:2368
	s_nop 3
	v_mul_f32_e32 v14, 0x3e000000, v30
	v_mul_f32_e32 v15, 0x3e000000, v31
	v_max3_f32 v26, v34, v14, v15
	v_mul_f32_e32 v27, 0x3e000000, v32
	s_waitcnt lgkmcnt(1)
	v_mfma_f32_16x16x32_bf16 v[14:17], v[22:25], v[6:9], 0
	v_mul_f32_e32 v22, 0x3e000000, v33
	v_max3_f32 v26, v26, v27, v22
	ds_read_b128 v[22:25], v88 offset:4608
	s_waitcnt lgkmcnt(1)
	v_mfma_f32_16x16x32_bf16 v[34:37], v[10:13], v[2:5], v[14:17]
	ds_read_b128 v[10:13], v88 offset:4672
	s_nop 6
	v_mul_f32_e32 v14, 0x3e000000, v34
	v_mul_f32_e32 v15, 0x3e000000, v35
	v_max3_f32 v26, v26, v14, v15
	s_waitcnt lgkmcnt(1)
	v_mfma_f32_16x16x32_bf16 v[14:17], v[22:25], v[6:9], 0
	v_mul_f32_e32 v27, 0x3e000000, v36
	v_mul_f32_e32 v28, 0x3e000000, v37
	v_max3_f32 v87, v26, v27, v28
	s_waitcnt lgkmcnt(0)
	v_mfma_f32_16x16x32_bf16 v[26:29], v[10:13], v[2:5], v[14:17]
	ds_read_b128 v[22:25], v88 offset:6912
	ds_read_b128 v[170:173], v88 offset:6976
	s_waitcnt vmcnt(5)
	ds_write_b128 v75, v[18:21] offset:18432
	s_waitcnt vmcnt(4)
	ds_write_b128 v75, v[158:161] offset:27648
	s_waitcnt lgkmcnt(0)
	s_nop 0
	v_mul_f32_e32 v10, 0x3e000000, v26
	v_mul_f32_e32 v11, 0x3e000000, v27
	v_max3_f32 v14, v87, v10, v11
	v_mfma_f32_16x16x32_bf16 v[10:13], v[22:25], v[6:9], 0
	v_mul_f32_e32 v15, 0x3e000000, v28
	v_mul_f32_e32 v16, 0x3e000000, v29
	v_max3_f32 v14, v14, v15, v16
	v_mfma_f32_16x16x32_bf16 v[22:25], v[170:173], v[2:5], v[10:13]
	s_barrier
; #define LAS __attribute__((address_space(3)))
; __device__ __forceinline__ unsigned cvt_pk_bf16(float lo, float hi) { const float __attribute__((ext_vector_type(2))) v = {lo, hi}; return __builtin_bit_cast(unsigned, __builtin_convertvector(v, bf16x2_t)); }
; template <bool LOCAL>
; __device__ __forceinline__ void na_unit(const bf16* P, const bf16* VT, bf16* YCAT, const LAS float* rpb_l, LAS bf16* buf, int b, int gr, int hp, int qblk, int tid) {
;     ...
;             if (sidx == NCH - 1) { m = fmaxf(m, __shfl_xor(m, 16)); m = fmaxf(m, __shfl_xor(m, 32)); }
;         } else {
;             const int c = sidx - NCH;
;             if (LOCAL && c < 8) {
;                 float p[8];
; #pragma unroll
;                 for (int e = 0; e < 4; ++e) { p[e] = __expf(sl[2 * (c < 8 ? c : 0)][e] - m); p[4 + e] = __expf(sl[2 * (c < 8 ? c : 0) + 1][e] - m); }
; #pragma unroll
;                 for (int e = 0; e < 8; ++e) lsum += p[e];
;                 const bf16x8 pf = __builtin_bit_cast(bf16x8, (v4u){pg8::cvt_pk_bf16(p[0], p[1]), pg8::cvt_pk_bf16(p[2], p[3]), pg8::cvt_pk_bf16(p[4], p[5]), pg8::cvt_pk_bf16(p[6], p[7])});
; #pragma unroll
;                 for (int dt = 0; dt < 4; ++dt) { const LAS bf16* vp = cb + (16 * dt + fr) * 72 + kc0 + 4 * fq;
;                     o[dt] = __builtin_amdgcn_mfma_f32_16x16x32_bf16(frag44(vp, vp + 16), pf, o[dt], 0, 0, 0); }
	v_lshl_add_u64 v[18:19], s[16:17], 1, v[78:79]
	v_lshl_add_u64 v[20:21], v[18:19], 0, v[70:71]
	v_lshl_add_u64 v[18:19], v[18:19], 0, v[80:81]
	s_nop 3
	v_mul_f32_e32 v10, 0x3e000000, v22
	v_mul_f32_e32 v11, 0x3e000000, v23
	v_max3_f32 v14, v14, v10, v11
	ds_read_b128 v[10:13], v88 offset:18432
	v_mul_f32_e32 v15, 0x3e000000, v24
	v_mul_f32_e32 v16, 0x3e000000, v25
	v_max3_f32 v87, v14, v15, v16
	ds_read_b128 v[14:17], v88 offset:18496
	s_waitcnt lgkmcnt(1)
	v_mfma_f32_16x16x32_bf16 v[10:13], v[10:13], v[6:9], 0
	v_lshl_add_u64 v[248:249], v[20:21], 0, 0
	v_lshl_add_u64 v[238:239], v[18:19], 0, 0
	global_load_dwordx4 v[158:161], v[20:21], off
	global_load_dwordx4 v[170:173], v[18:19], off
	global_load_dword v250, v[248:249], off offset:128
	global_load_dword v251, v[238:239], off offset:128
	ds_read_b128 v[18:21], v88 offset:20736
	ds_read_b128 v[174:177], v88 offset:23040
	s_waitcnt lgkmcnt(2)
	v_mfma_f32_16x16x32_bf16 v[14:17], v[14:17], v[2:5], v[10:13]
	s_nop 2
	ds_read_b128 v[10:13], v88 offset:20800
	s_waitcnt lgkmcnt(2)
	v_mfma_f32_16x16x32_bf16 v[18:21], v[18:21], v[6:9], 0
	s_nop 1
	v_mul_f32_e32 v130, 0x3e000000, v14
	v_mul_f32_e32 v135, 0x3e000000, v15
	v_max3_f32 v87, v87, v130, v135
	s_waitcnt lgkmcnt(0)
	v_mfma_f32_16x16x32_bf16 v[18:21], v[10:13], v[2:5], v[18:21]
	ds_read_b128 v[10:13], v88 offset:23104
	ds_read_b128 v[178:181], v88 offset:25344
	ds_read_b128 v[182:185], v88 offset:25408
	v_mul_f32_e32 v130, 0x3e000000, v16
	v_mfma_f32_16x16x32_bf16 v[174:177], v[174:177], v[6:9], 0
	v_mul_f32_e32 v135, 0x3e000000, v17
	v_max3_f32 v87, v87, v130, v135
	s_nop 0
	v_mul_f32_e32 v130, 0x3e000000, v18
	s_waitcnt lgkmcnt(1)
	v_mfma_f32_16x16x32_bf16 v[6:9], v[178:181], v[6:9], 0
	v_mul_f32_e32 v135, 0x3e000000, v19
	v_max3_f32 v87, v87, v130, v135
	v_mul_f32_e32 v130, 0x3e000000, v20
	v_mfma_f32_16x16x32_bf16 v[10:13], v[10:13], v[2:5], v[174:177]
	v_mul_f32_e32 v135, 0x3e000000, v21
	v_max3_f32 v87, v87, v130, v135
	s_waitcnt vmcnt(7)
	ds_write_b128 v75, v[162:165]
	s_waitcnt vmcnt(6)
	ds_write_b128 v75, v[166:169] offset:9216
	s_waitcnt lgkmcnt(2)
	v_mfma_f32_16x16x32_bf16 v[2:5], v[182:185], v[2:5], v[6:9]
	v_mul_f32_e32 v88, 0x3e000000, v10
	v_mul_f32_e32 v130, 0x3e000000, v11
	v_max3_f32 v87, v87, v88, v130
	v_mul_f32_e32 v88, 0x3e000000, v12
	v_mul_f32_e32 v130, 0x3e000000, v13
	v_max3_f32 v87, v87, v88, v130
	s_nop 1
	v_mul_f32_e32 v6, 0x3e000000, v2
	v_mul_f32_e32 v7, 0x3e000000, v3
	v_max3_f32 v6, v87, v6, v7
	v_mul_f32_e32 v7, 0x3e000000, v4
	v_mul_f32_e32 v8, 0x3e000000, v5
	v_max3_f32 v6, v6, v7, v8
	v_cndmask_b32_e32 v7, v1, v82, vcc
	v_lshlrev_b32_e32 v87, 2, v7
	ds_bpermute_b32 v7, v87, v6
	v_cmp_lt_i32_e32 vcc, v84, v83
	v_lshl_add_u32 v8, v89, 1, v155
	v_lshl_add_u64 v[182:183], s[14:15], 1, v[78:79]
	v_lshl_add_u64 v[184:185], v[182:183], 0, v[70:71]
	s_waitcnt lgkmcnt(0)
	v_max_f32_e32 v7, v7, v7
	v_max_f32_e32 v6, v6, v7
	v_cndmask_b32_e32 v7, v1, v84, vcc
	v_lshlrev_b32_e32 v88, 2, v7
	ds_bpermute_b32 v7, v88, v6
	v_lshl_add_u64 v[186:187], v[182:183], 0, v[80:81]
	s_waitcnt lgkmcnt(0)
	s_barrier
	v_max_f32_e32 v7, v7, v7
	v_max_f32_e32 v135, v6, v7
	v_sub_f32_e32 v6, v91, v135
	v_mul_f32_e32 v6, 0x3fb8aa3b, v6
	v_exp_f32_e32 v130, v6
	v_sub_f32_e32 v6, v95, v135
	v_mul_f32_e32 v6, 0x3fb8aa3b, v6
	v_exp_f32_e32 v91, v6
	v_sub_f32_e32 v6, v90, v135
	v_mul_f32_e32 v6, 0x3fb8aa3b, v6
	v_exp_f32_e32 v95, v6
	v_sub_f32_e32 v6, v94, v135
	v_mul_f32_e32 v6, 0x3fb8aa3b, v6
	v_exp_f32_e32 v90, v6
	v_sub_f32_e32 v6, v93, v135
	v_mul_f32_e32 v6, 0x3fb8aa3b, v6
	v_exp_f32_e32 v94, v6
	v_sub_f32_e32 v6, v98, v135
	v_mul_f32_e32 v6, 0x3fb8aa3b, v6
	v_exp_f32_e32 v93, v6
	v_sub_f32_e32 v6, v92, v135
	v_mul_f32_e32 v6, 0x3fb8aa3b, v6
	v_exp_f32_e32 v98, v6
	v_sub_f32_e32 v6, v96, v135
	v_mul_f32_e32 v6, 0x3fb8aa3b, v6
	v_exp_f32_e32 v92, v6
	v_add_u32_e32 v7, 0x800, v8
	v_add_u32_e32 v6, 0x1000, v8
	ds_read2_b64 v[162:165], v8 offset1:4
	ds_read2_b64 v[174:177], v7 offset0:32 offset1:36
	ds_read2_b64 v[178:181], v6 offset0:64 offset1:68
	v_lshl_add_u64 v[248:249], v[184:185], 0, 0
	v_lshl_add_u64 v[238:239], v[186:187], 0, 0
	global_load_dwordx4 v[182:185], v[184:185], off
	s_nop 0
	global_load_dwordx4 v[186:189], v[186:187], off
	global_load_dword v250, v[248:249], off offset:128
	global_load_dword v251, v[238:239], off offset:128
	v_sub_f32_e32 v9, v99, v135
	v_mul_f32_e32 v9, 0x3fb8aa3b, v9
	v_add_u32_e32 v157, 0x1800, v8
	v_exp_f32_e32 v85, v9
	v_sub_f32_e32 v9, v104, v135
	ds_read2_b64 v[190:193], v157 offset0:96 offset1:100
	v_mul_f32_e32 v9, 0x3fb8aa3b, v9
	v_exp_f32_e32 v76, v9
	v_sub_f32_e32 v9, v97, v135
	v_mul_f32_e32 v9, 0x3fb8aa3b, v9
	v_exp_f32_e32 v89, v9
	v_sub_f32_e32 v9, v102, v135
	v_mul_f32_e32 v9, 0x3fb8aa3b, v9
	v_exp_f32_e32 v86, v9
	v_sub_f32_e32 v9, v101, v135
	v_mul_f32_e32 v9, 0x3fb8aa3b, v9
	v_exp_f32_e32 v97, v9
	v_sub_f32_e32 v9, v108, v135
	v_cvt_pk_bf16_f32 v166, v130, v95
	v_cvt_pk_bf16_f32 v167, v94, v98
	v_cvt_pk_bf16_f32 v168, v91, v90
	v_cvt_pk_bf16_f32 v169, v93, v92
	s_waitcnt vmcnt(7)
	ds_write_b128 v75, v[158:161] offset:18432
	s_waitcnt vmcnt(6)
	ds_write_b128 v75, v[170:173] offset:27648
	v_mul_f32_e32 v9, 0x3fb8aa3b, v9
	v_add_u32_e32 v159, 0x4800, v8
	v_add_u32_e32 v158, 0x5000, v8
	s_waitcnt lgkmcnt(5)
	v_mfma_f32_16x16x32_bf16 v[162:165], v[162:165], v[166:169], 0
	s_waitcnt lgkmcnt(0)
	s_barrier
; #define LAS __attribute__((address_space(3)))
; __device__ __forceinline__ unsigned cvt_pk_bf16(float lo, float hi) { const float __attribute__((ext_vector_type(2))) v = {lo, hi}; return __builtin_bit_cast(unsigned, __builtin_convertvector(v, bf16x2_t)); }
; template <bool LOCAL>
; __device__ __forceinline__ void na_unit(const bf16* P, const bf16* VT, bf16* YCAT, const LAS float* rpb_l, LAS bf16* buf, int b, int gr, int hp, int qblk, int tid) {
;     ...
;             if (LOCAL && c < 8) {
;                 float p[8];
; #pragma unroll
;                 for (int e = 0; e < 4; ++e) { p[e] = __expf(sl[2 * (c < 8 ? c : 0)][e] - m); p[4 + e] = __expf(sl[2 * (c < 8 ? c : 0) + 1][e] - m); }
; #pragma unroll
;                 for (int e = 0; e < 8; ++e) lsum += p[e];
;                 const bf16x8 pf = __builtin_bit_cast(bf16x8, (v4u){pg8::cvt_pk_bf16(p[0], p[1]), pg8::cvt_pk_bf16(p[2], p[3]), pg8::cvt_pk_bf16(p[4], p[5]), pg8::cvt_pk_bf16(p[6], p[7])});
; #pragma unroll
;                 for (int dt = 0; dt < 4; ++dt) { const LAS bf16* vp = cb + (16 * dt + fr) * 72 + kc0 + 4 * fq;
;                     o[dt] = __builtin_amdgcn_mfma_f32_16x16x32_bf16(frag44(vp, vp + 16), pf, o[dt], 0, 0, 0); }
	v_mfma_f32_16x16x32_bf16 v[174:177], v[174:177], v[166:169], 0
	v_exp_f32_e32 v96, v9
	v_sub_f32_e32 v9, v100, v135
	ds_read2_b64 v[170:173], v159 offset1:4
	v_mfma_f32_16x16x32_bf16 v[178:181], v[178:181], v[166:169], 0
	v_mul_f32_e32 v9, 0x3fb8aa3b, v9
	v_exp_f32_e32 v99, v9
	v_sub_f32_e32 v9, v106, v135
	v_mfma_f32_16x16x32_bf16 v[166:169], v[190:193], v[166:169], 0
	ds_read2_b64 v[190:193], v158 offset0:32 offset1:36
	v_mul_f32_e32 v9, 0x3fb8aa3b, v9
	v_exp_f32_e32 v100, v9
	v_lshl_add_u64 v[160:161], s[0:1], 1, v[78:79]
	v_cvt_pk_bf16_f32 v194, v85, v89
	v_cvt_pk_bf16_f32 v195, v97, v99
	v_cvt_pk_bf16_f32 v196, v76, v86
	v_cvt_pk_bf16_f32 v197, v96, v100
	v_lshl_add_u64 v[198:199], v[160:161], 0, v[70:71]
	v_lshl_add_u64 v[200:201], v[160:161], 0, v[80:81]
	v_add_u32_e32 v160, 0x5800, v8
	s_waitcnt lgkmcnt(1)
	v_mfma_f32_16x16x32_bf16 v[162:165], v[170:173], v[194:197], v[162:165]
	v_sub_f32_e32 v9, v105, v135
	v_mul_f32_e32 v9, 0x3fb8aa3b, v9
	v_add_u32_e32 v161, 0x6000, v8
	s_waitcnt lgkmcnt(0)
	v_mfma_f32_16x16x32_bf16 v[170:173], v[190:193], v[194:197], v[174:177]
	v_exp_f32_e32 v102, v9
	v_sub_f32_e32 v9, v112, v135
	v_mul_f32_e32 v9, 0x3fb8aa3b, v9
	ds_read2_b64 v[174:177], v160 offset0:64 offset1:68
	v_lshl_add_u64 v[248:249], v[198:199], 0, 0
	v_lshl_add_u64 v[238:239], v[200:201], 0, 0
	global_load_dwordx4 v[190:193], v[198:199], off
	s_nop 0
	global_load_dwordx4 v[198:201], v[200:201], off
	global_load_dword v250, v[248:249], off offset:128
	global_load_dword v251, v[238:239], off offset:128
	s_waitcnt lgkmcnt(0)
	v_mfma_f32_16x16x32_bf16 v[174:177], v[174:177], v[194:197], v[178:181]
	s_nop 2
	ds_read2_b64 v[178:181], v161 offset0:96 offset1:100
	v_exp_f32_e32 v101, v9
	v_sub_f32_e32 v9, v103, v135
	v_mul_f32_e32 v9, 0x3fb8aa3b, v9
	v_exp_f32_e32 v104, v9
	v_sub_f32_e32 v9, v110, v135
	v_mul_f32_e32 v9, 0x3fb8aa3b, v9
	v_exp_f32_e32 v103, v9
	v_sub_f32_e32 v9, v109, v135
	v_mul_f32_e32 v9, 0x3fb8aa3b, v9
	v_exp_f32_e32 v106, v9
	v_sub_f32_e32 v9, v115, v135
	v_mul_f32_e32 v9, 0x3fb8aa3b, v9
	s_waitcnt lgkmcnt(0)
	v_mfma_f32_16x16x32_bf16 v[166:169], v[178:181], v[194:197], v[166:169]
	s_waitcnt vmcnt(7)
	ds_write_b128 v75, v[182:185]
	s_waitcnt vmcnt(6)
	ds_write_b128 v75, v[186:189] offset:9216
	s_waitcnt lgkmcnt(0)
	s_barrier
	v_exp_f32_e32 v105, v9
	v_sub_f32_e32 v9, v107, v135
	ds_read2_b64 v[178:181], v8 offset1:4
	ds_read2_b64 v[182:185], v7 offset0:32 offset1:36
	v_mul_f32_e32 v9, 0x3fb8aa3b, v9
	v_exp_f32_e32 v107, v9
	v_sub_f32_e32 v9, v111, v135
	v_mul_f32_e32 v9, 0x3fb8aa3b, v9
	v_exp_f32_e32 v108, v9
	v_lshl_add_u64 v[194:195], s[18:19], 1, v[78:79]
	v_cvt_pk_bf16_f32 v186, v102, v104
	v_cvt_pk_bf16_f32 v187, v106, v107
	v_cvt_pk_bf16_f32 v188, v101, v103
	v_cvt_pk_bf16_f32 v189, v105, v108
	v_lshl_add_u64 v[110:111], v[194:195], 0, v[70:71]
	v_lshl_add_u64 v[194:195], v[194:195], 0, v[80:81]
	s_waitcnt lgkmcnt(1)
	v_mfma_f32_16x16x32_bf16 v[162:165], v[178:181], v[186:189], v[162:165]
	ds_read2_b64 v[178:181], v6 offset0:64 offset1:68
	v_sub_f32_e32 v9, v114, v135
	v_mul_f32_e32 v9, 0x3fb8aa3b, v9
	s_waitcnt lgkmcnt(1)
	v_mfma_f32_16x16x32_bf16 v[170:173], v[182:185], v[186:189], v[170:173]
	v_lshl_add_u64 v[248:249], v[110:111], 0, 0
	v_lshl_add_u64 v[238:239], v[194:195], 0, 0
	global_load_dwordx4 v[182:185], v[110:111], off
	s_nop 0
	global_load_dwordx4 v[194:197], v[194:195], off
	global_load_dword v250, v[248:249], off offset:128
	global_load_dword v251, v[238:239], off offset:128
	v_exp_f32_e32 v110, v9
	v_sub_f32_e32 v9, v120, v135
	s_waitcnt lgkmcnt(0)
	v_mfma_f32_16x16x32_bf16 v[174:177], v[178:181], v[186:189], v[174:177]
	ds_read2_b64 v[178:181], v157 offset0:96 offset1:100
	v_mul_f32_e32 v9, 0x3fb8aa3b, v9
	v_exp_f32_e32 v109, v9
	v_sub_f32_e32 v9, v113, v135
	v_mul_f32_e32 v9, 0x3fb8aa3b, v9
	v_exp_f32_e32 v112, v9
	v_sub_f32_e32 v9, v118, v135
	v_mul_f32_e32 v9, 0x3fb8aa3b, v9
	v_exp_f32_e32 v111, v9
	v_sub_f32_e32 v9, v117, v135
	v_mul_f32_e32 v9, 0x3fb8aa3b, v9
	v_exp_f32_e32 v114, v9
	v_sub_f32_e32 v9, v123, v135
	v_mul_f32_e32 v9, 0x3fb8aa3b, v9
	s_waitcnt lgkmcnt(0)
	v_mfma_f32_16x16x32_bf16 v[166:169], v[178:181], v[186:189], v[166:169]
	s_waitcnt vmcnt(7)
	ds_write_b128 v75, v[190:193] offset:18432
	s_waitcnt vmcnt(6)
	ds_write_b128 v75, v[198:201] offset:27648
	s_waitcnt lgkmcnt(0)
	s_barrier
	v_exp_f32_e32 v113, v9
	v_sub_f32_e32 v9, v116, v135
	ds_read2_b64 v[178:181], v159 offset1:4
	v_mul_f32_e32 v9, 0x3fb8aa3b, v9
	v_exp_f32_e32 v115, v9
	v_sub_f32_e32 v9, v119, v135
	v_mul_f32_e32 v9, 0x3fb8aa3b, v9
	v_exp_f32_e32 v116, v9
	v_lshl_add_u64 v[198:199], s[20:21], 1, v[78:79]
	v_lshl_add_u64 v[200:201], v[198:199], 0, v[70:71]
	ds_read2_b64 v[186:189], v158 offset0:32 offset1:36
	v_cvt_pk_bf16_f32 v190, v110, v112
	v_cvt_pk_bf16_f32 v191, v114, v115
	v_cvt_pk_bf16_f32 v192, v109, v111
	v_cvt_pk_bf16_f32 v193, v113, v116
	v_lshl_add_u64 v[118:119], v[198:199], 0, v[80:81]
	v_sub_f32_e32 v9, v122, v135
	s_waitcnt lgkmcnt(1)
	v_mfma_f32_16x16x32_bf16 v[162:165], v[178:181], v[190:193], v[162:165]
	v_lshl_add_u64 v[248:249], v[200:201], 0, 0
	v_lshl_add_u64 v[238:239], v[118:119], 0, 0
	global_load_dwordx4 v[178:181], v[200:201], off
	s_nop 0
	global_load_dwordx4 v[198:201], v[118:119], off
	global_load_dword v250, v[248:249], off offset:128
	global_load_dword v251, v[238:239], off offset:128
	v_mul_f32_e32 v9, 0x3fb8aa3b, v9
	v_exp_f32_e32 v118, v9
	s_waitcnt lgkmcnt(0)
	v_mfma_f32_16x16x32_bf16 v[170:173], v[186:189], v[190:193], v[170:173]
	ds_read2_b64 v[186:189], v160 offset0:64 offset1:68
	v_sub_f32_e32 v9, v128, v135
	v_mul_f32_e32 v9, 0x3fb8aa3b, v9
	s_waitcnt lgkmcnt(0)
	v_mfma_f32_16x16x32_bf16 v[174:177], v[186:189], v[190:193], v[174:177]
	ds_read2_b64 v[186:189], v161 offset0:96 offset1:100
	v_exp_f32_e32 v117, v9
	v_sub_f32_e32 v9, v121, v135
	v_mul_f32_e32 v9, 0x3fb8aa3b, v9
	v_exp_f32_e32 v120, v9
	v_sub_f32_e32 v9, v126, v135
	v_mul_f32_e32 v9, 0x3fb8aa3b, v9
	v_exp_f32_e32 v119, v9
	v_sub_f32_e32 v9, v125, v135
	v_mul_f32_e32 v9, 0x3fb8aa3b, v9
	v_exp_f32_e32 v122, v9
	v_sub_f32_e32 v9, v132, v135
	v_mul_f32_e32 v9, 0x3fb8aa3b, v9
	s_waitcnt lgkmcnt(0)
	v_mfma_f32_16x16x32_bf16 v[166:169], v[186:189], v[190:193], v[166:169]
	s_waitcnt vmcnt(7)
	ds_write_b128 v75, v[182:185]
	s_waitcnt vmcnt(6)
	ds_write_b128 v75, v[194:197] offset:9216
	s_waitcnt lgkmcnt(0)
	s_barrier
; #define LAS __attribute__((address_space(3)))
; __device__ __forceinline__ unsigned cvt_pk_bf16(float lo, float hi) { const float __attribute__((ext_vector_type(2))) v = {lo, hi}; return __builtin_bit_cast(unsigned, __builtin_convertvector(v, bf16x2_t)); }
; template <bool LOCAL>
; __device__ __forceinline__ void na_unit(const bf16* P, const bf16* VT, bf16* YCAT, const LAS float* rpb_l, LAS bf16* buf, int b, int gr, int hp, int qblk, int tid) {
;     ...
;             if (LOCAL && c < 8) {
;                 float p[8];
; #pragma unroll
;                 for (int e = 0; e < 4; ++e) { p[e] = __expf(sl[2 * (c < 8 ? c : 0)][e] - m); p[4 + e] = __expf(sl[2 * (c < 8 ? c : 0) + 1][e] - m); }
; #pragma unroll
;                 for (int e = 0; e < 8; ++e) lsum += p[e];
;                 const bf16x8 pf = __builtin_bit_cast(bf16x8, (v4u){pg8::cvt_pk_bf16(p[0], p[1]), pg8::cvt_pk_bf16(p[2], p[3]), pg8::cvt_pk_bf16(p[4], p[5]), pg8::cvt_pk_bf16(p[6], p[7])});
; #pragma unroll
;                 for (int dt = 0; dt < 4; ++dt) { const LAS bf16* vp = cb + (16 * dt + fr) * 72 + kc0 + 4 * fq;
;                     o[dt] = __builtin_amdgcn_mfma_f32_16x16x32_bf16(frag44(vp, vp + 16), pf, o[dt], 0, 0, 0); }
;             } else {
;                 const int cc = c - NLOC;
; #pragma unroll
;                 for (int p2 = 0; p2 < 2; ++p2) {
;                     float p[8];
; #pragma unroll
;                     for (int e = 0; e < 4; ++e) { p[e] = __expf(sc[4 * (cc >= 0 ? cc : 0) + 2 * p2][e] - m); p[4 + e] = __expf(sc[4 * (cc >= 0 ? cc : 0) + 2 * p2 + 1][e] - m); }
; #pragma unroll
;                     for (int e = 0; e < 8; ++e) lsum += p[e];
;                     const bf16x8 pf = __builtin_bit_cast(bf16x8, (v4u){pg8::cvt_pk_bf16(p[0], p[1]), pg8::cvt_pk_bf16(p[2], p[3]), pg8::cvt_pk_bf16(p[4], p[5]), pg8::cvt_pk_bf16(p[6], p[7])});
; #pragma unroll
;                     for (int dt = 0; dt < 4; ++dt) { const LAS bf16* vp = cb + (16 * dt + fr) * 72 + 32 * p2 + 4 * fq;
;                         o[dt] = __builtin_amdgcn_mfma_f32_16x16x32_bf16(frag44(vp, vp + 16), pf, o[dt], 0, 0, 0); }
;                 }
	v_exp_f32_e32 v121, v9
	v_sub_f32_e32 v9, v124, v135
	ds_read2_b64 v[182:185], v8 offset1:4
	ds_read2_b64 v[186:189], v7 offset0:32 offset1:36
	v_mul_f32_e32 v9, 0x3fb8aa3b, v9
	v_exp_f32_e32 v123, v9
	v_sub_f32_e32 v9, v127, v135
	v_mul_f32_e32 v9, 0x3fb8aa3b, v9
	v_exp_f32_e32 v124, v9
	v_lshl_add_u64 v[194:195], s[22:23], 1, v[78:79]
	v_cvt_pk_bf16_f32 v190, v118, v120
	v_cvt_pk_bf16_f32 v191, v122, v123
	v_cvt_pk_bf16_f32 v192, v117, v119
	v_cvt_pk_bf16_f32 v193, v121, v124
	v_lshl_add_u64 v[126:127], v[194:195], 0, v[70:71]
	v_lshl_add_u64 v[194:195], v[194:195], 0, v[80:81]
	s_waitcnt lgkmcnt(1)
	v_mfma_f32_16x16x32_bf16 v[162:165], v[182:185], v[190:193], v[162:165]
	ds_read2_b64 v[182:185], v6 offset0:64 offset1:68
	v_sub_f32_e32 v9, v131, v135
	v_mul_f32_e32 v9, 0x3fb8aa3b, v9
	s_waitcnt lgkmcnt(1)
	v_mfma_f32_16x16x32_bf16 v[170:173], v[186:189], v[190:193], v[170:173]
	v_lshl_add_u64 v[248:249], v[126:127], 0, 0
	v_lshl_add_u64 v[238:239], v[194:195], 0, 0
	global_load_dwordx4 v[186:189], v[126:127], off
	s_nop 0
	global_load_dwordx4 v[194:197], v[194:195], off
	global_load_dword v250, v[248:249], off offset:128
	global_load_dword v251, v[238:239], off offset:128
	v_exp_f32_e32 v126, v9
	v_sub_f32_e32 v9, v138, v135
	v_mul_f32_e32 v9, 0x3fb8aa3b, v9
	v_exp_f32_e32 v125, v9
	v_sub_f32_e32 v9, v129, v135
	v_mul_f32_e32 v9, 0x3fb8aa3b, v9
	v_exp_f32_e32 v128, v9
	v_sub_f32_e32 v9, v136, v135
	v_mul_f32_e32 v9, 0x3fb8aa3b, v9
	v_exp_f32_e32 v127, v9
	v_sub_f32_e32 v9, v134, v135
	v_mul_f32_e32 v9, 0x3fb8aa3b, v9
	v_exp_f32_e32 v131, v9
	v_sub_f32_e32 v9, v141, v135
	s_waitcnt lgkmcnt(0)
	v_mfma_f32_16x16x32_bf16 v[174:177], v[182:185], v[190:193], v[174:177]
	ds_read2_b64 v[182:185], v157 offset0:96 offset1:100
	v_mul_f32_e32 v9, 0x3fb8aa3b, v9
	s_waitcnt vmcnt(7)
	ds_write_b128 v75, v[178:181] offset:18432
	s_waitcnt vmcnt(6)
	ds_write_b128 v75, v[198:201] offset:27648
	s_waitcnt lgkmcnt(0)
	s_barrier
	v_exp_f32_e32 v129, v9
	v_sub_f32_e32 v9, v133, v135
	ds_read2_b64 v[178:181], v159 offset1:4
	v_mul_f32_e32 v9, 0x3fb8aa3b, v9
	v_exp_f32_e32 v132, v9
	v_sub_f32_e32 v9, v137, v135
	v_mul_f32_e32 v9, 0x3fb8aa3b, v9
	v_exp_f32_e32 v133, v9
	v_lshl_add_u64 v[198:199], s[24:25], 1, v[78:79]
	v_mfma_f32_16x16x32_bf16 v[166:169], v[182:185], v[190:193], v[166:169]
	v_lshl_add_u64 v[200:201], v[198:199], 0, v[70:71]
	ds_read2_b64 v[182:185], v158 offset0:32 offset1:36
	v_cvt_pk_bf16_f32 v190, v126, v128
	v_cvt_pk_bf16_f32 v191, v131, v132
	v_cvt_pk_bf16_f32 v192, v125, v127
	v_cvt_pk_bf16_f32 v193, v129, v133
	v_lshl_add_u64 v[136:137], v[198:199], 0, v[80:81]
	v_sub_f32_e32 v9, v140, v135
	s_waitcnt lgkmcnt(1)
	v_mfma_f32_16x16x32_bf16 v[162:165], v[178:181], v[190:193], v[162:165]
	global_load_dwordx4 v[178:181], v[200:201], off
	s_nop 0
	global_load_dwordx4 v[198:201], v[136:137], off
	v_mul_f32_e32 v9, 0x3fb8aa3b, v9
	v_exp_f32_e32 v136, v9
	s_waitcnt lgkmcnt(0)
	v_mfma_f32_16x16x32_bf16 v[170:173], v[182:185], v[190:193], v[170:173]
	ds_read2_b64 v[182:185], v160 offset0:64 offset1:68
	v_sub_f32_e32 v9, v146, v135
	v_mul_f32_e32 v9, 0x3fb8aa3b, v9
	s_waitcnt lgkmcnt(0)
	v_mfma_f32_16x16x32_bf16 v[174:177], v[182:185], v[190:193], v[174:177]
	ds_read2_b64 v[182:185], v161 offset0:96 offset1:100
	v_exp_f32_e32 v134, v9
	v_sub_f32_e32 v9, v139, v135
	v_mul_f32_e32 v9, 0x3fb8aa3b, v9
	v_exp_f32_e32 v138, v9
	v_sub_f32_e32 v9, v144, v135
	v_mul_f32_e32 v9, 0x3fb8aa3b, v9
	v_exp_f32_e32 v137, v9
	v_sub_f32_e32 v9, v143, v135
	v_mul_f32_e32 v9, 0x3fb8aa3b, v9
	s_waitcnt lgkmcnt(0)
	v_mfma_f32_16x16x32_bf16 v[166:169], v[182:185], v[190:193], v[166:169]
	s_waitcnt vmcnt(5)
	ds_write_b128 v75, v[186:189]
	s_waitcnt vmcnt(4)
	ds_write_b128 v75, v[194:197] offset:9216
	s_waitcnt lgkmcnt(0)
	s_barrier
	v_exp_f32_e32 v140, v9
	v_sub_f32_e32 v9, v149, v135
	ds_read2_b64 v[182:185], v8 offset1:4
	v_mul_f32_e32 v9, 0x3fb8aa3b, v9
	ds_read2_b64 v[190:193], v7 offset0:32 offset1:36
	v_exp_f32_e32 v139, v9
	v_sub_f32_e32 v9, v142, v135
	v_sub_f32_e32 v8, v145, v135
	v_mul_f32_e32 v9, 0x3fb8aa3b, v9
	v_mul_f32_e32 v8, 0x3fb8aa3b, v8
	v_exp_f32_e32 v141, v9
	v_exp_f32_e32 v142, v8
	v_cvt_pk_bf16_f32 v186, v136, v138
	v_cvt_pk_bf16_f32 v188, v134, v137
	v_cvt_pk_bf16_f32 v187, v140, v141
	v_cvt_pk_bf16_f32 v189, v139, v142
	v_lshl_add_u64 v[8:9], s[26:27], 1, v[78:79]
	v_sub_f32_e32 v144, v150, v135
	s_waitcnt lgkmcnt(1)
	v_mfma_f32_16x16x32_bf16 v[162:165], v[182:185], v[186:189], v[162:165]
	ds_read2_b64 v[182:185], v6 offset0:64 offset1:68
	v_lshl_add_u64 v[6:7], v[8:9], 0, v[70:71]
	v_lshl_add_u64 v[8:9], v[8:9], 0, v[80:81]
	s_waitcnt lgkmcnt(1)
	v_mfma_f32_16x16x32_bf16 v[170:173], v[190:193], v[186:189], v[170:173]
	v_lshl_add_u64 v[248:249], v[6:7], 0, 0
	v_lshl_add_u64 v[238:239], v[8:9], 0, 0
	global_load_dwordx4 v[190:193], v[6:7], off
	global_load_dwordx4 v[194:197], v[8:9], off
	global_load_dword v250, v[248:249], off offset:128
	global_load_dword v251, v[238:239], off offset:128
	ds_read2_b64 v[78:81], v157 offset0:96 offset1:100
	s_waitcnt vmcnt(5)
	ds_write_b128 v75, v[178:181] offset:18432
	s_waitcnt vmcnt(4)
	ds_write_b128 v75, v[198:201] offset:27648
	s_waitcnt lgkmcnt(2)
	v_mfma_f32_16x16x32_bf16 v[166:169], v[78:81], v[186:189], v[166:169]
	s_waitcnt lgkmcnt(0)
	s_barrier
; #define LAS __attribute__((address_space(3)))
; __device__ __forceinline__ unsigned cvt_pk_bf16(float lo, float hi) { const float __attribute__((ext_vector_type(2))) v = {lo, hi}; return __builtin_bit_cast(unsigned, __builtin_convertvector(v, bf16x2_t)); }
; template <bool LOCAL>
; __device__ __forceinline__ void na_unit(const bf16* P, const bf16* VT, bf16* YCAT, const LAS float* rpb_l, LAS bf16* buf, int b, int gr, int hp, int qblk, int tid) {
;     ...
;             } else {
;                 const int cc = c - NLOC;
; #pragma unroll
;                 for (int p2 = 0; p2 < 2; ++p2) {
;                     float p[8];
; #pragma unroll
;                     for (int e = 0; e < 4; ++e) { p[e] = __expf(sc[4 * (cc >= 0 ? cc : 0) + 2 * p2][e] - m); p[4 + e] = __expf(sc[4 * (cc >= 0 ? cc : 0) + 2 * p2 + 1][e] - m); }
; #pragma unroll
;                     for (int e = 0; e < 8; ++e) lsum += p[e];
;                     const bf16x8 pf = __builtin_bit_cast(bf16x8, (v4u){pg8::cvt_pk_bf16(p[0], p[1]), pg8::cvt_pk_bf16(p[2], p[3]), pg8::cvt_pk_bf16(p[4], p[5]), pg8::cvt_pk_bf16(p[6], p[7])});
; #pragma unroll
;                     for (int dt = 0; dt < 4; ++dt) { const LAS bf16* vp = cb + (16 * dt + fr) * 72 + 32 * p2 + 4 * fq;
;                         o[dt] = __builtin_amdgcn_mfma_f32_16x16x32_bf16(frag44(vp, vp + 16), pf, o[dt], 0, 0, 0); }
;                 }
	v_sub_f32_e32 v70, v148, v135
	v_sub_f32_e32 v79, v147, v135
	v_sub_f32_e32 v81, v151, v135
	ds_read2_b64 v[146:149], v159 offset1:4
	v_mul_f32_e32 v70, 0x3fb8aa3b, v70
	v_mul_f32_e32 v79, 0x3fb8aa3b, v79
	v_mul_f32_e32 v81, 0x3fb8aa3b, v81
	v_mul_f32_e32 v144, 0x3fb8aa3b, v144
	v_exp_f32_e32 v78, v70
	v_sub_f32_e32 v70, v154, v135
	v_exp_f32_e32 v80, v79
	v_sub_f32_e32 v79, v152, v135
	v_exp_f32_e32 v143, v81
	v_sub_f32_e32 v81, v156, v135
	v_exp_f32_e32 v145, v144
	v_sub_f32_e32 v144, v153, v135
	v_mul_f32_e32 v70, 0x3fb8aa3b, v70
	v_mul_f32_e32 v79, 0x3fb8aa3b, v79
	v_mul_f32_e32 v81, 0x3fb8aa3b, v81
	v_mul_f32_e32 v144, 0x3fb8aa3b, v144
	v_exp_f32_e32 v70, v70
	v_exp_f32_e32 v79, v79
	v_exp_f32_e32 v81, v81
	v_exp_f32_e32 v144, v144
	v_cvt_pk_bf16_f32 v150, v78, v80
	v_cvt_pk_bf16_f32 v151, v143, v145
	v_cvt_pk_bf16_f32 v152, v70, v79
	v_cvt_pk_bf16_f32 v153, v81, v144
	v_mfma_f32_16x16x32_bf16 v[174:177], v[182:185], v[186:189], v[174:177]
	v_fma_f32 v62, v62, s71, -v135
	v_fma_f32 v63, v63, s71, -v135
	v_fma_f32 v64, v64, s71, -v135
	s_waitcnt lgkmcnt(0)
	v_mfma_f32_16x16x32_bf16 v[162:165], v[146:149], v[150:153], v[162:165]
	ds_read2_b64 v[146:149], v158 offset0:32 offset1:36
	v_fma_f32 v65, v65, s71, -v135
	v_mul_f32_e32 v62, 0x3fb8aa3b, v62
	s_waitcnt lgkmcnt(0)
	v_mfma_f32_16x16x32_bf16 v[156:159], v[146:149], v[150:153], v[170:173]
	ds_read2_b64 v[146:149], v160 offset0:64 offset1:68
	v_mul_f32_e32 v63, 0x3fb8aa3b, v63
	v_mul_f32_e32 v64, 0x3fb8aa3b, v64
	s_waitcnt lgkmcnt(0)
	v_mfma_f32_16x16x32_bf16 v[170:173], v[146:149], v[150:153], v[174:177]
	ds_read2_b64 v[146:149], v161 offset0:96 offset1:100
	s_nop 1
	v_lshl_add_u64 v[248:249], v[6:7], 0, 0
	v_lshl_add_u64 v[238:239], v[8:9], 0, 0
	global_load_dwordx4 v[174:177], v[6:7], off offset:128
	global_load_dwordx4 v[178:181], v[8:9], off offset:128
	global_load_dword v250, v[248:249], off offset:256
	global_load_dword v251, v[238:239], off offset:256
	s_waitcnt vmcnt(7)
	ds_write_b128 v75, v[190:193]
	s_waitcnt vmcnt(6)
	ds_write_b128 v75, v[194:197] offset:9216
	s_waitcnt lgkmcnt(2)
	v_mfma_f32_16x16x32_bf16 v[148:151], v[146:149], v[150:153], v[166:169]
	s_waitcnt lgkmcnt(0)
	s_barrier
	s_nop 0
	ds_read2_b64 v[166:169], v155 offset1:4
	v_mul_f32_e32 v65, 0x3fb8aa3b, v65
	v_exp_f32_e32 v146, v62
	v_fma_f32 v62, v66, s71, -v135
	v_exp_f32_e32 v66, v63
	v_fma_f32 v63, v67, s71, -v135
	v_exp_f32_e32 v67, v64
	v_fma_f32 v64, v68, s71, -v135
	v_exp_f32_e32 v68, v65
	v_fma_f32 v65, v69, s71, -v135
	v_mul_f32_e32 v62, 0x3fb8aa3b, v62
	v_mul_f32_e32 v63, 0x3fb8aa3b, v63
	v_mul_f32_e32 v64, 0x3fb8aa3b, v64
	v_mul_f32_e32 v65, 0x3fb8aa3b, v65
	v_exp_f32_e32 v62, v62
	v_exp_f32_e32 v63, v63
	v_exp_f32_e32 v64, v64
	v_exp_f32_e32 v65, v65
	v_cvt_pk_bf16_f32 v182, v146, v66
	v_cvt_pk_bf16_f32 v183, v67, v68
	v_cvt_pk_bf16_f32 v184, v62, v63
	v_cvt_pk_bf16_f32 v185, v64, v65
	v_add_u32_e32 v147, 0x800, v155
	v_add_u32_e32 v152, 0x1000, v155
	s_waitcnt lgkmcnt(0)
	v_mfma_f32_16x16x32_bf16 v[160:163], v[166:169], v[182:185], v[162:165]
	v_add_u32_e32 v153, 0x1800, v155
	v_fma_f32 v58, v58, s71, -v135
	v_fma_f32 v54, v54, s71, -v135
	ds_read2_b64 v[164:167], v147 offset0:32 offset1:36
	s_waitcnt lgkmcnt(0)
	v_mfma_f32_16x16x32_bf16 v[156:159], v[164:167], v[182:185], v[156:159]
	ds_read2_b64 v[164:167], v152 offset0:64 offset1:68
	v_fma_f32 v59, v59, s71, -v135
	v_fma_f32 v55, v55, s71, -v135
	s_waitcnt lgkmcnt(0)
	v_mfma_f32_16x16x32_bf16 v[164:167], v[164:167], v[182:185], v[170:173]
	s_nop 2
	ds_read2_b64 v[168:171], v153 offset0:96 offset1:100
	v_fma_f32 v60, v60, s71, -v135
	v_fma_f32 v56, v56, s71, -v135
	s_waitcnt lgkmcnt(0)
	v_mfma_f32_16x16x32_bf16 v[148:151], v[168:171], v[182:185], v[148:151]
	ds_read2_b64 v[168:171], v155 offset0:8 offset1:12
	v_fma_f32 v61, v61, s71, -v135
	v_fma_f32 v57, v57, s71, -v135
	v_mul_f32_e32 v58, 0x3fb8aa3b, v58
	v_mul_f32_e32 v54, 0x3fb8aa3b, v54
	v_mul_f32_e32 v59, 0x3fb8aa3b, v59
	v_mul_f32_e32 v55, 0x3fb8aa3b, v55
	v_mul_f32_e32 v60, 0x3fb8aa3b, v60
	v_mul_f32_e32 v56, 0x3fb8aa3b, v56
	v_mul_f32_e32 v61, 0x3fb8aa3b, v61
	v_mul_f32_e32 v57, 0x3fb8aa3b, v57
	v_exp_f32_e32 v58, v58
	v_exp_f32_e32 v54, v54
	v_exp_f32_e32 v59, v59
	v_exp_f32_e32 v55, v55
	v_exp_f32_e32 v60, v60
	v_exp_f32_e32 v56, v56
	v_exp_f32_e32 v61, v61
	v_exp_f32_e32 v57, v57
	v_cvt_pk_bf16_f32 v182, v58, v59
	v_cvt_pk_bf16_f32 v184, v54, v55
	v_cvt_pk_bf16_f32 v183, v60, v61
	v_cvt_pk_bf16_f32 v185, v56, v57
	v_fma_f32 v46, v46, s71, -v135
	v_fma_f32 v47, v47, s71, -v135
	s_waitcnt lgkmcnt(0)
	v_mfma_f32_16x16x32_bf16 v[160:163], v[168:171], v[182:185], v[160:163]
	ds_read2_b64 v[168:171], v147 offset0:40 offset1:44
	v_fma_f32 v48, v48, s71, -v135
	v_mul_f32_e32 v46, 0x3fb8aa3b, v46
	s_waitcnt lgkmcnt(0)
	v_mfma_f32_16x16x32_bf16 v[156:159], v[168:171], v[182:185], v[156:159]
	ds_read2_b64 v[168:171], v152 offset0:72 offset1:76
	v_mul_f32_e32 v47, 0x3fb8aa3b, v47
	v_mul_f32_e32 v48, 0x3fb8aa3b, v48
	s_waitcnt lgkmcnt(0)
	v_mfma_f32_16x16x32_bf16 v[164:167], v[168:171], v[182:185], v[164:167]
	ds_read2_b64 v[168:171], v153 offset0:104 offset1:108
	v_exp_f32_e32 v69, v46
	v_fma_f32 v46, v50, s71, -v135
	v_exp_f32_e32 v50, v47
	v_fma_f32 v47, v51, s71, -v135
	v_exp_f32_e32 v51, v48
	v_fma_f32 v48, v52, s71, -v135
	v_add_u32_e32 v52, 0x4800, v155
	v_lshl_add_u64 v[248:249], v[6:7], 0, 0
	v_lshl_add_u64 v[238:239], v[8:9], 0, 0
	global_load_dwordx4 v[186:189], v[6:7], off offset:256
	global_load_dwordx4 v[190:193], v[8:9], off offset:256
	global_load_dword v250, v[248:249], off offset:384
	global_load_dword v251, v[238:239], off offset:384
	s_waitcnt lgkmcnt(0)
	v_mfma_f32_16x16x32_bf16 v[148:151], v[168:171], v[182:185], v[148:151]
	s_waitcnt vmcnt(7)
	ds_write_b128 v75, v[174:177] offset:18432
	s_waitcnt vmcnt(6)
	ds_write_b128 v75, v[178:181] offset:27648
	s_waitcnt lgkmcnt(0)
	s_barrier
; #define LAS __attribute__((address_space(3)))
; __device__ __forceinline__ unsigned cvt_pk_bf16(float lo, float hi) { const float __attribute__((ext_vector_type(2))) v = {lo, hi}; return __builtin_bit_cast(unsigned, __builtin_convertvector(v, bf16x2_t)); }
; template <bool LOCAL>
; __device__ __forceinline__ void na_unit(const bf16* P, const bf16* VT, bf16* YCAT, const LAS float* rpb_l, LAS bf16* buf, int b, int gr, int hp, int qblk, int tid) {
;     ...
;             } else {
;                 const int cc = c - NLOC;
; #pragma unroll
;                 for (int p2 = 0; p2 < 2; ++p2) {
;                     float p[8];
; #pragma unroll
;                     for (int e = 0; e < 4; ++e) { p[e] = __expf(sc[4 * (cc >= 0 ? cc : 0) + 2 * p2][e] - m); p[4 + e] = __expf(sc[4 * (cc >= 0 ? cc : 0) + 2 * p2 + 1][e] - m); }
; #pragma unroll
;                     for (int e = 0; e < 8; ++e) lsum += p[e];
;                     const bf16x8 pf = __builtin_bit_cast(bf16x8, (v4u){pg8::cvt_pk_bf16(p[0], p[1]), pg8::cvt_pk_bf16(p[2], p[3]), pg8::cvt_pk_bf16(p[4], p[5]), pg8::cvt_pk_bf16(p[6], p[7])});
; #pragma unroll
;                     for (int dt = 0; dt < 4; ++dt) { const LAS bf16* vp = cb + (16 * dt + fr) * 72 + 32 * p2 + 4 * fq;
;                         o[dt] = __builtin_amdgcn_mfma_f32_16x16x32_bf16(frag44(vp, vp + 16), pf, o[dt], 0, 0, 0); }
;                 }
	v_fma_f32 v49, v49, s71, -v135
	ds_read2_b64 v[168:171], v52 offset1:4
	v_mul_f32_e32 v49, 0x3fb8aa3b, v49
	v_exp_f32_e32 v154, v49
	v_fma_f32 v49, v53, s71, -v135
	v_mul_f32_e32 v46, 0x3fb8aa3b, v46
	v_mul_f32_e32 v47, 0x3fb8aa3b, v47
	v_mul_f32_e32 v48, 0x3fb8aa3b, v48
	v_mul_f32_e32 v49, 0x3fb8aa3b, v49
	v_exp_f32_e32 v46, v46
	v_exp_f32_e32 v47, v47
	v_exp_f32_e32 v48, v48
	v_exp_f32_e32 v53, v49
	v_cvt_pk_bf16_f32 v172, v69, v50
	v_cvt_pk_bf16_f32 v173, v51, v154
	v_cvt_pk_bf16_f32 v174, v46, v47
	v_cvt_pk_bf16_f32 v175, v48, v53
	v_add_u32_e32 v176, 0x5000, v155
	v_add_u32_e32 v177, 0x5800, v155
	s_waitcnt lgkmcnt(0)
	v_mfma_f32_16x16x32_bf16 v[160:163], v[168:171], v[172:175], v[160:163]
	ds_read2_b64 v[168:171], v176 offset0:32 offset1:36
	v_add_u32_e32 v49, 0x6000, v155
	v_fma_f32 v38, v38, s71, -v135
	s_waitcnt lgkmcnt(0)
	v_mfma_f32_16x16x32_bf16 v[156:159], v[168:171], v[172:175], v[156:159]
	ds_read2_b64 v[168:171], v177 offset0:64 offset1:68
	v_mul_f32_e32 v38, 0x3fb8aa3b, v38
	v_fma_f32 v42, v42, s71, -v135
	s_waitcnt lgkmcnt(0)
	v_mfma_f32_16x16x32_bf16 v[164:167], v[168:171], v[172:175], v[164:167]
	ds_read2_b64 v[168:171], v49 offset0:96 offset1:100
	v_mul_f32_e32 v42, 0x3fb8aa3b, v42
	v_fma_f32 v30, v30, s71, -v135
	s_waitcnt lgkmcnt(0)
	v_mfma_f32_16x16x32_bf16 v[148:151], v[168:171], v[172:175], v[148:151]
	v_exp_f32_e32 v173, v38
	v_fma_f32 v38, v43, s71, -v135
	v_mul_f32_e32 v38, 0x3fb8aa3b, v38
	v_exp_f32_e32 v174, v38
	v_fma_f32 v38, v39, s71, -v135
	v_mul_f32_e32 v38, 0x3fb8aa3b, v38
	v_exp_f32_e32 v175, v38
	v_fma_f32 v38, v44, s71, -v135
	v_mul_f32_e32 v38, 0x3fb8aa3b, v38
	v_exp_f32_e32 v178, v38
	v_fma_f32 v38, v40, s71, -v135
	v_mul_f32_e32 v38, 0x3fb8aa3b, v38
	v_exp_f32_e32 v172, v42
	v_exp_f32_e32 v179, v38
	v_fma_f32 v38, v45, s71, -v135
	ds_read2_b64 v[42:45], v52 offset0:8 offset1:12
	v_mul_f32_e32 v38, 0x3fb8aa3b, v38
	v_exp_f32_e32 v180, v38
	v_fma_f32 v38, v41, s71, -v135
	v_mul_f32_e32 v38, 0x3fb8aa3b, v38
	v_exp_f32_e32 v181, v38
	v_cvt_pk_bf16_f32 v38, v172, v174
	v_cvt_pk_bf16_f32 v39, v178, v180
	v_cvt_pk_bf16_f32 v40, v173, v175
	v_cvt_pk_bf16_f32 v41, v179, v181
	v_mul_f32_e32 v30, 0x3fb8aa3b, v30
	v_fma_f32 v22, v22, s71, -v135
	s_waitcnt lgkmcnt(0)
	v_mfma_f32_16x16x32_bf16 v[42:45], v[42:45], v[38:41], v[160:163]
	v_mul_f32_e32 v22, 0x3fb8aa3b, v22
	v_fma_f32 v26, v26, s71, -v135
	v_mul_f32_e32 v26, 0x3fb8aa3b, v26
	ds_read2_b64 v[160:163], v176 offset0:40 offset1:44
	s_waitcnt lgkmcnt(0)
	v_mfma_f32_16x16x32_bf16 v[156:159], v[160:163], v[38:41], v[156:159]
	ds_read2_b64 v[160:163], v177 offset0:72 offset1:76
	v_fma_f32 v2, v2, s71, -v135
	v_mul_f32_e32 v2, 0x3fb8aa3b, v2
	s_waitcnt lgkmcnt(0)
	v_mfma_f32_16x16x32_bf16 v[160:163], v[160:163], v[38:41], v[164:167]
	s_nop 2
	ds_read2_b64 v[164:167], v49 offset0:104 offset1:108
	global_load_dwordx4 v[168:171], v[6:7], off offset:384
	s_nop 0
	global_load_dwordx4 v[6:9], v[8:9], off offset:384
	s_waitcnt vmcnt(5)
	ds_write_b128 v75, v[186:189]
	s_waitcnt vmcnt(4)
	ds_write_b128 v75, v[190:193] offset:9216
	s_waitcnt lgkmcnt(2)
	v_mfma_f32_16x16x32_bf16 v[38:41], v[164:167], v[38:41], v[148:151]
	v_exp_f32_e32 v164, v30
	v_fma_f32 v30, v34, s71, -v135
	v_mul_f32_e32 v30, 0x3fb8aa3b, v30
	v_exp_f32_e32 v165, v30
	v_fma_f32 v30, v31, s71, -v135
	v_mul_f32_e32 v30, 0x3fb8aa3b, v30
	v_exp_f32_e32 v166, v30
	v_fma_f32 v30, v35, s71, -v135
	v_mul_f32_e32 v30, 0x3fb8aa3b, v30
	v_exp_f32_e32 v167, v30
	v_fma_f32 v30, v32, s71, -v135
	v_mul_f32_e32 v30, 0x3fb8aa3b, v30
	v_exp_f32_e32 v182, v30
	v_fma_f32 v30, v36, s71, -v135
	v_mul_f32_e32 v30, 0x3fb8aa3b, v30
	v_exp_f32_e32 v183, v30
	v_fma_f32 v30, v33, s71, -v135
	s_waitcnt lgkmcnt(0)
	s_barrier
	v_mul_f32_e32 v34, 0x3fb8aa3b, v30
	ds_read2_b64 v[30:33], v155 offset1:4
	v_exp_f32_e32 v184, v34
	v_fma_f32 v34, v37, s71, -v135
	v_mul_f32_e32 v34, 0x3fb8aa3b, v34
	v_exp_f32_e32 v185, v34
	v_cvt_pk_bf16_f32 v34, v164, v166
	v_cvt_pk_bf16_f32 v35, v182, v184
	v_cvt_pk_bf16_f32 v36, v165, v167
	v_cvt_pk_bf16_f32 v37, v183, v185
	ds_read2_b64 v[148:151], v152 offset0:64 offset1:68
	v_fma_f32 v10, v10, s71, -v135
	s_waitcnt lgkmcnt(1)
	v_mfma_f32_16x16x32_bf16 v[30:33], v[30:33], v[34:37], v[42:45]
	v_mul_f32_e32 v10, 0x3fb8aa3b, v10
	s_nop 1
	ds_read2_b64 v[42:45], v147 offset0:32 offset1:36
	s_waitcnt lgkmcnt(0)
	v_mfma_f32_16x16x32_bf16 v[42:45], v[42:45], v[34:37], v[156:159]
	s_nop 2
	ds_read2_b64 v[156:159], v153 offset0:96 offset1:100
	v_mfma_f32_16x16x32_bf16 v[148:151], v[148:151], v[34:37], v[160:163]
	s_waitcnt lgkmcnt(0)
	v_mfma_f32_16x16x32_bf16 v[34:37], v[156:159], v[34:37], v[38:41]
	v_exp_f32_e32 v157, v22
	v_fma_f32 v22, v27, s71, -v135
	v_mul_f32_e32 v22, 0x3fb8aa3b, v22
	v_exp_f32_e32 v158, v22
	v_fma_f32 v22, v23, s71, -v135
	v_mul_f32_e32 v22, 0x3fb8aa3b, v22
	v_exp_f32_e32 v159, v22
	v_fma_f32 v22, v28, s71, -v135
	v_mul_f32_e32 v22, 0x3fb8aa3b, v22
	v_exp_f32_e32 v160, v22
	v_fma_f32 v22, v24, s71, -v135
	v_mul_f32_e32 v22, 0x3fb8aa3b, v22
	v_exp_f32_e32 v156, v26
	v_exp_f32_e32 v161, v22
	v_fma_f32 v22, v29, s71, -v135
	ds_read2_b64 v[26:29], v155 offset0:8 offset1:12
	v_mul_f32_e32 v22, 0x3fb8aa3b, v22
	v_exp_f32_e32 v155, v22
	v_fma_f32 v22, v25, s71, -v135
	v_mul_f32_e32 v22, 0x3fb8aa3b, v22
	v_exp_f32_e32 v162, v22
	v_cvt_pk_bf16_f32 v22, v156, v158
	v_cvt_pk_bf16_f32 v23, v160, v155
	v_cvt_pk_bf16_f32 v24, v157, v159
	v_cvt_pk_bf16_f32 v25, v161, v162
	ds_read2_b64 v[38:41], v152 offset0:72 offset1:76
	s_waitcnt lgkmcnt(1)
	v_mfma_f32_16x16x32_bf16 v[26:29], v[26:29], v[22:25], v[30:33]
	s_nop 2
	ds_read2_b64 v[30:33], v147 offset0:40 offset1:44
	s_waitcnt lgkmcnt(0)
	v_mfma_f32_16x16x32_bf16 v[30:33], v[30:33], v[22:25], v[42:45]
	s_nop 2
	ds_read2_b64 v[42:45], v153 offset0:104 offset1:108
	s_waitcnt vmcnt(1)
	ds_write_b128 v75, v[168:171] offset:18432
	s_waitcnt vmcnt(0)
	ds_write_b128 v75, v[6:9] offset:27648
	v_fma_f32 v6, v14, s71, -v135
	v_mul_f32_e32 v6, 0x3fb8aa3b, v6
	v_mfma_f32_16x16x32_bf16 v[38:41], v[38:41], v[22:25], v[148:151]
	s_waitcnt lgkmcnt(0)
	s_barrier
; #define LAS __attribute__((address_space(3)))
; __device__ __forceinline__ unsigned cvt_pk_bf16(float lo, float hi) { const float __attribute__((ext_vector_type(2))) v = {lo, hi}; return __builtin_bit_cast(unsigned, __builtin_convertvector(v, bf16x2_t)); }
; #define NA_STORE(sidx) do { LAS bf16* d_ = buf + ((sidx) & 1) * 9216; _Pragma("unroll") for (int q_ = 0; q_ < 2; ++q_) *(LAS v4u*)(d_ + q_ * 4608 + lrow * 72 + lseg * 8) = ld[(sidx) & 1][q_]; } while (0)
; template <bool LOCAL>
; __device__ __forceinline__ void na_unit(const bf16* P, const bf16* VT, bf16* YCAT, const LAS float* rpb_l, LAS bf16* buf, int b, int gr, int hp, int qblk, int tid) {
;     ...
;                     for (int e = 0; e < 4; ++e) { p[e] = __expf(sc[4 * (cc >= 0 ? cc : 0) + 2 * p2][e] - m); p[4 + e] = __expf(sc[4 * (cc >= 0 ? cc : 0) + 2 * p2 + 1][e] - m); }
; #pragma unroll
;                     for (int e = 0; e < 8; ++e) lsum += p[e];
;                     const bf16x8 pf = __builtin_bit_cast(bf16x8, (v4u){pg8::cvt_pk_bf16(p[0], p[1]), pg8::cvt_pk_bf16(p[2], p[3]), pg8::cvt_pk_bf16(p[4], p[5]), pg8::cvt_pk_bf16(p[6], p[7])});
; #pragma unroll
;                     for (int dt = 0; dt < 4; ++dt) { const LAS bf16* vp = cb + (16 * dt + fr) * 72 + 32 * p2 + 4 * fq;
;                         o[dt] = __builtin_amdgcn_mfma_f32_16x16x32_bf16(frag44(vp, vp + 16), pf, o[dt], 0, 0, 0); }
;                 }
;             }
;         }
;         if (sidx + 1 < 2 * NCH) NA_STORE(sidx + 1);
;         __syncthreads();
;     }
;     ...
;     lsum += __shfl_xor(lsum, 16); lsum += __shfl_xor(lsum, 32);
	v_mfma_f32_16x16x32_bf16 v[22:25], v[42:45], v[22:25], v[34:37]
	v_ashrrev_i32_e32 v75, 31, v74
	s_nop 1
	v_exp_f32_e32 v34, v6
	v_fma_f32 v6, v18, s71, -v135
	v_mul_f32_e32 v6, 0x3fb8aa3b, v6
	v_exp_f32_e32 v35, v6
	v_fma_f32 v6, v15, s71, -v135
	v_mul_f32_e32 v6, 0x3fb8aa3b, v6
	v_exp_f32_e32 v36, v6
	v_fma_f32 v6, v19, s71, -v135
	v_mul_f32_e32 v6, 0x3fb8aa3b, v6
	v_exp_f32_e32 v37, v6
	v_fma_f32 v6, v16, s71, -v135
	v_mul_f32_e32 v6, 0x3fb8aa3b, v6
	v_exp_f32_e32 v42, v6
	v_fma_f32 v6, v20, s71, -v135
	v_mul_f32_e32 v6, 0x3fb8aa3b, v6
	v_exp_f32_e32 v43, v6
	v_fma_f32 v6, v17, s71, -v135
	v_mul_f32_e32 v14, 0x3fb8aa3b, v6
	ds_read2_b64 v[6:9], v52 offset1:4
	v_exp_f32_e32 v44, v14
	v_fma_f32 v14, v21, s71, -v135
	v_mul_f32_e32 v14, 0x3fb8aa3b, v14
	v_exp_f32_e32 v45, v14
	v_cvt_pk_bf16_f32 v14, v34, v36
	v_cvt_pk_bf16_f32 v15, v42, v44
	v_cvt_pk_bf16_f32 v16, v35, v37
	v_cvt_pk_bf16_f32 v17, v43, v45
	ds_read2_b64 v[18:21], v176 offset0:32 offset1:36
	s_waitcnt lgkmcnt(1)
	v_mfma_f32_16x16x32_bf16 v[6:9], v[6:9], v[14:17], v[26:29]
	s_nop 2
	ds_read2_b64 v[26:29], v177 offset0:64 offset1:68
	s_waitcnt lgkmcnt(0)
	v_mfma_f32_16x16x32_bf16 v[26:29], v[26:29], v[14:17], v[38:41]
	s_nop 2
	v_add_f32_e32 v38, 0, v130
	v_add_f32_e32 v38, v95, v38
	v_add_f32_e32 v38, v94, v38
	v_add_f32_e32 v38, v98, v38
	v_add_f32_e32 v38, v91, v38
	v_add_f32_e32 v38, v90, v38
	v_add_f32_e32 v38, v93, v38
	v_add_f32_e32 v38, v92, v38
	v_add_f32_e32 v38, v85, v38
	v_add_f32_e32 v38, v89, v38
	v_add_f32_e32 v38, v97, v38
	v_add_f32_e32 v38, v99, v38
	v_add_f32_e32 v38, v76, v38
	v_add_f32_e32 v38, v86, v38
	v_add_f32_e32 v38, v96, v38
	v_add_f32_e32 v38, v100, v38
	v_add_f32_e32 v38, v102, v38
	v_add_f32_e32 v38, v104, v38
	v_add_f32_e32 v38, v106, v38
	v_add_f32_e32 v38, v107, v38
	v_add_f32_e32 v38, v101, v38
	v_add_f32_e32 v38, v103, v38
	v_add_f32_e32 v38, v105, v38
	v_add_f32_e32 v38, v108, v38
	v_add_f32_e32 v38, v110, v38
	v_add_f32_e32 v38, v112, v38
	v_add_f32_e32 v38, v114, v38
	v_add_f32_e32 v38, v115, v38
	v_add_f32_e32 v38, v109, v38
	v_add_f32_e32 v38, v111, v38
	v_add_f32_e32 v38, v113, v38
	v_add_f32_e32 v38, v116, v38
	v_add_f32_e32 v38, v118, v38
	v_add_f32_e32 v38, v120, v38
	v_add_f32_e32 v38, v122, v38
	v_add_f32_e32 v38, v123, v38
	v_add_f32_e32 v38, v117, v38
	v_add_f32_e32 v38, v119, v38
	v_add_f32_e32 v38, v121, v38
	v_add_f32_e32 v38, v124, v38
	v_add_f32_e32 v38, v126, v38
	v_add_f32_e32 v38, v128, v38
	v_add_f32_e32 v38, v131, v38
	v_add_f32_e32 v38, v132, v38
	v_add_f32_e32 v38, v125, v38
	v_add_f32_e32 v38, v127, v38
	v_add_f32_e32 v38, v129, v38
	v_add_f32_e32 v38, v133, v38
	v_add_f32_e32 v38, v136, v38
	v_add_f32_e32 v38, v138, v38
	v_add_f32_e32 v38, v140, v38
	v_add_f32_e32 v38, v141, v38
	v_add_f32_e32 v38, v134, v38
	v_add_f32_e32 v38, v137, v38
	v_add_f32_e32 v38, v139, v38
	v_add_f32_e32 v38, v142, v38
	v_add_f32_e32 v38, v78, v38
	v_add_f32_e32 v38, v80, v38
	v_add_f32_e32 v38, v143, v38
	v_add_f32_e32 v38, v145, v38
	v_add_f32_e32 v38, v70, v38
	v_add_f32_e32 v38, v79, v38
	v_add_f32_e32 v38, v81, v38
	v_add_f32_e32 v38, v144, v38
	v_add_f32_e32 v38, v146, v38
	v_add_f32_e32 v38, v66, v38
	v_add_f32_e32 v38, v67, v38
	v_add_f32_e32 v38, v68, v38
	v_add_f32_e32 v38, v62, v38
	v_add_f32_e32 v38, v63, v38
	v_add_f32_e32 v38, v64, v38
	v_add_f32_e32 v38, v65, v38
	v_add_f32_e32 v38, v58, v38
	v_add_f32_e32 v38, v59, v38
	v_add_f32_e32 v38, v60, v38
	v_add_f32_e32 v38, v61, v38
	v_add_f32_e32 v38, v54, v38
	v_add_f32_e32 v38, v55, v38
	v_add_f32_e32 v38, v56, v38
	v_add_f32_e32 v38, v57, v38
	v_add_f32_e32 v38, v69, v38
	v_add_f32_e32 v38, v50, v38
	v_add_f32_e32 v38, v51, v38
	v_add_f32_e32 v38, v154, v38
	v_add_f32_e32 v38, v46, v38
	v_add_f32_e32 v38, v47, v38
	v_add_f32_e32 v38, v48, v38
	v_add_f32_e32 v38, v53, v38
	v_add_f32_e32 v38, v172, v38
	v_mfma_f32_16x16x32_bf16 v[18:21], v[18:21], v[14:17], v[30:33]
	v_add_f32_e32 v38, v174, v38
	v_add_f32_e32 v38, v178, v38
	v_add_f32_e32 v38, v180, v38
	ds_read2_b64 v[30:33], v49 offset0:96 offset1:100
	v_add_f32_e32 v38, v173, v38
	v_add_f32_e32 v38, v175, v38
	v_add_f32_e32 v38, v179, v38
	v_add_f32_e32 v38, v181, v38
	v_add_f32_e32 v38, v164, v38
	v_add_f32_e32 v38, v166, v38
	s_waitcnt lgkmcnt(0)
	v_mfma_f32_16x16x32_bf16 v[14:17], v[30:33], v[14:17], v[22:25]
	v_add_f32_e32 v38, v182, v38
	s_nop 1
	v_exp_f32_e32 v23, v2
	v_fma_f32 v2, v11, s71, -v135
	v_mul_f32_e32 v2, 0x3fb8aa3b, v2
	v_add_f32_e32 v38, v184, v38
	v_exp_f32_e32 v24, v2
	v_fma_f32 v2, v3, s71, -v135
	v_add_f32_e32 v38, v165, v38
	v_mul_f32_e32 v2, 0x3fb8aa3b, v2
	v_add_f32_e32 v38, v167, v38
	v_exp_f32_e32 v25, v2
	v_fma_f32 v2, v12, s71, -v135
	v_add_f32_e32 v38, v183, v38
	v_mul_f32_e32 v2, 0x3fb8aa3b, v2
	v_add_f32_e32 v38, v185, v38
	v_exp_f32_e32 v30, v2
	v_fma_f32 v2, v4, s71, -v135
	v_add_f32_e32 v38, v156, v38
	v_mul_f32_e32 v2, 0x3fb8aa3b, v2
	v_add_f32_e32 v38, v158, v38
	v_exp_f32_e32 v22, v10
	v_exp_f32_e32 v31, v2
	v_fma_f32 v2, v13, s71, -v135
	ds_read2_b64 v[10:13], v52 offset0:8 offset1:12
	v_add_f32_e32 v38, v160, v38
	v_mul_f32_e32 v2, 0x3fb8aa3b, v2
	v_add_f32_e32 v38, v155, v38
	v_exp_f32_e32 v32, v2
	v_fma_f32 v2, v5, s71, -v135
	v_add_f32_e32 v38, v157, v38
	v_mul_f32_e32 v2, 0x3fb8aa3b, v2
	v_add_f32_e32 v38, v159, v38
	v_exp_f32_e32 v33, v2
	v_add_f32_e32 v38, v161, v38
	v_add_f32_e32 v38, v162, v38
	v_add_f32_e32 v34, v34, v38
	v_add_f32_e32 v34, v36, v34
	v_cvt_pk_bf16_f32 v2, v22, v24
	v_cvt_pk_bf16_f32 v3, v30, v32
	v_cvt_pk_bf16_f32 v4, v23, v25
	v_cvt_pk_bf16_f32 v5, v31, v33
	v_add_f32_e32 v34, v42, v34
	v_add_f32_e32 v34, v44, v34
	s_waitcnt lgkmcnt(0)
	v_mfma_f32_16x16x32_bf16 v[6:9], v[10:13], v[2:5], v[6:9]
	ds_read2_b64 v[10:13], v176 offset0:40 offset1:44
	v_add_f32_e32 v34, v35, v34
	v_add_f32_e32 v34, v37, v34
	v_add_f32_e32 v34, v43, v34
	v_add_f32_e32 v34, v45, v34
	v_add_f32_e32 v22, v22, v34
	v_add_f32_e32 v22, v24, v22
	v_add_f32_e32 v22, v30, v22
	v_add_f32_e32 v22, v32, v22
	s_waitcnt lgkmcnt(0)
	v_mfma_f32_16x16x32_bf16 v[10:13], v[10:13], v[2:5], v[18:21]
	v_add_f32_e32 v22, v23, v22
	v_add_f32_e32 v22, v25, v22
	v_add_f32_e32 v22, v31, v22
	ds_read2_b64 v[18:21], v177 offset0:72 offset1:76
	v_add_f32_e32 v30, v33, v22
	ds_bpermute_b32 v31, v87, v30
	ds_read2_b64 v[22:25], v49 offset0:104 offset1:108
	s_waitcnt lgkmcnt(2)
	v_mfma_f32_16x16x32_bf16 v[18:21], v[18:21], v[2:5], v[26:29]
	s_waitcnt lgkmcnt(1)
	s_nop 1
	v_add_f32_e32 v26, v30, v31
	ds_bpermute_b32 v27, v88, v26
	v_lshlrev_b32_e32 v70, 1, v77
	s_waitcnt lgkmcnt(1)
	v_mfma_f32_16x16x32_bf16 v[14:17], v[22:25], v[2:5], v[14:17]
	s_waitcnt lgkmcnt(0)
	s_barrier
; __device__ __forceinline__ unsigned cvt_pk_bf16(float lo, float hi) { const float __attribute__((ext_vector_type(2))) v = {lo, hi}; return __builtin_bit_cast(unsigned, __builtin_convertvector(v, bf16x2_t)); }
; template <bool LOCAL>
; __device__ __forceinline__ void na_unit(const bf16* P, const bf16* VT, bf16* YCAT, const LAS float* rpb_l, LAS bf16* buf, int b, int gr, int hp, int qblk, int tid) {
;     ...
;     lsum += __shfl_xor(lsum, 16); lsum += __shfl_xor(lsum, 32);
;     const float inv = 1.f / lsum;
;     bf16* op = YCAT + (size_t)(qrow0 + fr) * D + 512 + h * 64 + 4 * fq;
; #pragma unroll
;     for (int dt = 0; dt < 4; ++dt) { v2u w; w.x = pg8::cvt_pk_bf16(o[dt][0] * inv, o[dt][1] * inv); w.y = pg8::cvt_pk_bf16(o[dt][2] * inv, o[dt][3] * inv); *(v2u*)(op + dt * 16) = w; }
	v_add_f32_e32 v2, v26, v27
	v_div_scale_f32 v3, s[0:1], v2, v2, 1.0
	v_rcp_f32_e32 v4, v3
	s_nop 0
	v_fma_f32 v5, -v3, v4, 1.0
	v_fmac_f32_e32 v4, v5, v4
	v_div_scale_f32 v5, vcc, 1.0, v2, 1.0
	v_mul_f32_e32 v22, v5, v4
	v_fma_f32 v23, -v3, v22, v5
	v_fmac_f32_e32 v22, v23, v4
	v_fma_f32 v3, -v3, v22, v5
	v_div_fmas_f32 v3, v3, v4, v22
	v_div_fixup_f32 v22, v3, v2, 1.0
	v_lshlrev_b64 v[2:3], 11, v[74:75]
	v_lshl_add_u64 v[2:3], s[10:11], 0, v[2:3]
	v_lshl_add_u64 v[2:3], v[72:73], 1, v[2:3]
	v_pk_mul_f32 v[6:7], v[6:7], v[22:23] op_sel_hi:[1,0]
	v_pk_mul_f32 v[8:9], v[8:9], v[22:23] op_sel_hi:[1,0]
	v_lshl_add_u64 v[4:5], v[2:3], 0, v[70:71]
	v_cvt_pk_bf16_f32 v6, v6, v7
	v_cvt_pk_bf16_f32 v7, v8, v9
	global_store_dwordx2 v[4:5], v[6:7], off offset:1024
	v_pk_mul_f32 v[6:7], v[10:11], v[22:23] op_sel_hi:[1,0]
	v_pk_mul_f32 v[8:9], v[12:13], v[22:23] op_sel_hi:[1,0]
	v_cvt_pk_bf16_f32 v6, v6, v7
	v_cvt_pk_bf16_f32 v7, v8, v9
	global_store_dwordx2 v[4:5], v[6:7], off offset:1056
	v_pk_mul_f32 v[6:7], v[18:19], v[22:23] op_sel_hi:[1,0]
	v_pk_mul_f32 v[8:9], v[20:21], v[22:23] op_sel_hi:[1,0]
	v_cvt_pk_bf16_f32 v6, v6, v7
	v_cvt_pk_bf16_f32 v7, v8, v9
	v_lshl_add_u64 v[2:3], v[4:5], 0, s[12:13]
	global_store_dwordx2 v[4:5], v[6:7], off offset:1088
	v_pk_mul_f32 v[4:5], v[14:15], v[22:23] op_sel_hi:[1,0]
	v_pk_mul_f32 v[6:7], v[16:17], v[22:23] op_sel_hi:[1,0]
	v_cvt_pk_bf16_f32 v4, v4, v5

; template <bool LOCAL>
; __device__ __forceinline__ void na_unit(const bf16* P, const bf16* VT, bf16* YCAT, const LAS float* rpb_l, LAS bf16* buf, int b, int gr, int hp, int qblk, int tid) {
;     ...
;     v4u ld[2][2];
;     const int lrow = (tid >> 3) & 63, lseg = tid & 7;
;     ...
;     bf16x8 qf[2];
; #pragma unroll
;     for (int ks = 0; ks < 2; ++ks) qf[ks] = *(const bf16x8*)(P + (size_t)(qrow0 + fr) * DINP + h * 64 + 32 * ks + 8 * fq);
;     f32x4 sl[16], sc[16];
;     float m = -1.0e30f, lsum = 0.f;
;     f32x4 o[4];
; #pragma unroll
;     for (int dt = 0; dt < 4; ++dt) o[dt] = (f32x4){0.f, 0.f, 0.f, 0.f};
;     NA_ISSUE(0); NA_ISSUE(1); NA_STORE(0);
;     __syncthreads();
; #pragma unroll
;     for (int sidx = 0; sidx < 2 * NCH; ++sidx) {
;         if (sidx + 2 < 2 * NCH) NA_ISSUE(sidx + 2);
;         const LAS bf16* cb = buf + (sidx & 1) * 9216 + hh * 4608;
;         if (sidx < NCH) {
;             const int c = sidx;
;             if (LOCAL && c < 8) {
; #pragma unroll
;                 for (int t2 = 0; t2 < 2; ++t2) {
;                     const LAS bf16* kp = cb + (kc0 + 16 * t2 + fr) * 72 + 8 * fq;
;                     f32x4 acc = {0.f, 0.f, 0.f, 0.f};
;                     acc = __builtin_amdgcn_mfma_f32_16x16x32_bf16(*(const LAS bf16x8*)(kp), qf[0], acc, 0, 0, 0);
;                     acc = __builtin_amdgcn_mfma_f32_16x16x32_bf16(*(const LAS bf16x8*)(kp + 32), qf[1], acc, 0, 0, 0);
;                     const LAS float* rb = rpb + (r0 + c - gr + 7) * 31 + 15 - qcol;
; #pragma unroll
;                     for (int e = 0; e < 4; ++e) { const int kcol = kc0 + 16 * t2 + 4 * fq + e; const bool ok = (kcol >= cs) && (kcol < cs + 16);
;                         const float sv = ok ? acc[e] * 0.125f + rb[ok ? kcol : qcol] : -1.0e30f; acc[e] = sv; m = fmaxf(m, sv); }
;                     sl[2 * (c < 8 ? c : 0) + t2] = acc; }
;             } else {
;                 const int cc = c - NLOC;
; #pragma unroll
;                 for (int t4 = 0; t4 < 4; ++t4) {
;                     const LAS bf16* kp = cb + (16 * t4 + fr) * 72 + 8 * fq;
;                     f32x4 acc = {0.f, 0.f, 0.f, 0.f};
;                     acc = __builtin_amdgcn_mfma_f32_16x16x32_bf16(*(const LAS bf16x8*)(kp), qf[0], acc, 0, 0, 0);
;                     acc = __builtin_amdgcn_mfma_f32_16x16x32_bf16(*(const LAS bf16x8*)(kp + 32), qf[1], acc, 0, 0, 0);
; #pragma unroll
.LBB0_2650:
	v_mov_b32_e32 v94, v0
	s_movk_i32 s2, 0x2400
	v_and_b32_e32 v90, 15, v94
	v_bfe_u32 v92, v94, 4, 2
	v_ashrrev_i32_e32 v93, 8, v94
	s_mov_b64 s[0:1], -1
	s_cmpk_gt_i32 s80, 0x7ff
	v_bfe_u32 v89, v94, 3, 6
	v_lshlrev_b32_e32 v76, 3, v92
	v_lshlrev_b32_e32 v70, 4, v92
	v_mad_i32_i24 v87, v93, s2, 0
	v_mul_u32_u24_e32 v88, 0x90, v90
	s_waitcnt lgkmcnt(0)
	s_barrier
	s_cbranch_scc0 .LBB0_2652
	s_lshl_b32 s0, s80, 4
	s_and_b32 s0, s0, 0xffffff00
	s_addk_i32 s0, 0x8000
	v_mov_b64_e32 v[78:79], s[8:9]
	s_lshl_b32 s1, s80, 5
	v_or_b32_e32 v77, s0, v89
	v_lshlrev_b32_e32 v4, 4, v94
	s_and_b32 s16, s1, 0x180
	v_mad_u64_u32 v[2:3], s[14:15], v77, s72, v[78:79]
	v_and_b32_e32 v80, 0x70, v4
	v_mov_b32_e32 v81, v71
	v_lshl_add_u64 v[2:3], v[2:3], 0, v[80:81]
	s_lshl_b32 s2, s16, 1
	v_lshl_add_u64 v[2:3], v[2:3], 0, s[2:3]
	global_load_dwordx4 v[6:9], v[2:3], off offset:1024
	global_load_dwordx4 v[10:13], v[2:3], off offset:1152
	s_lshl_b32 s1, s80, 6
	s_and_b32 s1, s1, 0xc0
	v_lshrrev_b32_e32 v2, 2, v94
	v_and_or_b32 v2, v2, 48, s1
	v_lshl_add_u32 v4, v93, 6, s16
	v_or3_b32 v72, v2, v90, s0
	v_ashrrev_i32_e32 v5, 31, v4
	v_mad_u64_u32 v[2:3], s[14:15], v72, s72, v[78:79]
	v_lshlrev_b64 v[74:75], 1, v[4:5]
	v_lshl_add_u64 v[2:3], v[2:3], 0, v[74:75]
	v_or_b32_e32 v14, 64, v77
	v_lshl_add_u64 v[22:23], v[2:3], 0, v[70:71]
	v_mad_u64_u32 v[14:15], s[14:15], v14, s72, v[78:79]
	global_load_dwordx4 v[2:5], v[22:23], off
	v_lshl_add_u64 v[14:15], v[14:15], 0, v[80:81]
	v_lshl_add_u64 v[18:19], v[14:15], 0, s[2:3]
	s_mov_b32 s100, 0x60000
	s_mov_b32 s101, 0
	v_lshl_add_u64 v[248:249], v[18:19], 0, s[100:101]
	global_load_dwordx4 v[14:17], v[18:19], off offset:1024
	s_nop 0
	global_load_dwordx4 v[18:21], v[18:19], off offset:1152
	global_load_dword v250, v[248:249], off offset:1024
	global_load_dword v251, v[248:249], off offset:1152
	s_nop 0
	global_load_dwordx4 v[50:53], v[22:23], off offset:64
	v_mul_u32_u24_e32 v22, 0x90, v89
	v_add3_u32 v73, 0, v22, v80
	v_or_b32_e32 v22, 0x80, v77
	v_add3_u32 v91, v87, v70, v88
	s_mov_b32 s1, s3
	v_cmp_lt_i32_e32 vcc, v84, v85
	s_waitcnt vmcnt(7)
	ds_write_b128 v73, v[6:9]
	s_waitcnt vmcnt(6)
	ds_write_b128 v73, v[10:13] offset:9216
	v_mad_u64_u32 v[10:11], s[14:15], v22, s72, v[78:79]
	v_lshl_add_u64 v[10:11], v[10:11], 0, v[80:81]
	v_lshl_add_u64 v[26:27], v[10:11], 0, s[2:3]
	s_waitcnt lgkmcnt(0)
	s_barrier
	ds_read_b128 v[6:9], v91
	ds_read_b128 v[10:13], v91 offset:2304
	v_lshl_add_u64 v[248:249], v[26:27], 0, s[100:101]
	global_load_dwordx4 v[22:25], v[26:27], off offset:1024
	global_load_dwordx4 v[30:33], v[26:27], off offset:1152
	global_load_dword v250, v[248:249], off offset:1024
	global_load_dword v251, v[248:249], off offset:1152
	ds_read_b128 v[26:29], v91 offset:64
	ds_read_b128 v[34:37], v91 offset:4608
	ds_read_b128 v[38:41], v91 offset:2368
	ds_read_b128 v[42:45], v91 offset:4672
	ds_read_b128 v[46:49], v91 offset:6912
	s_waitcnt vmcnt(9) lgkmcnt(6)
	v_mfma_f32_16x16x32_bf16 v[6:9], v[6:9], v[2:5], 0
	ds_read_b128 v[54:57], v91 offset:6976
	s_waitcnt vmcnt(8)
	ds_write_b128 v73, v[14:17] offset:18432
	s_waitcnt vmcnt(7)
	ds_write_b128 v73, v[18:21] offset:27648
	s_waitcnt lgkmcnt(0)
	v_mfma_f32_16x16x32_bf16 v[10:13], v[10:13], v[2:5], 0
	s_barrier
	v_mfma_f32_16x16x32_bf16 v[14:17], v[34:37], v[2:5], 0
	v_mfma_f32_16x16x32_bf16 v[18:21], v[46:49], v[2:5], 0
	ds_read_b128 v[34:37], v91 offset:18432
	ds_read_b128 v[46:49], v91 offset:18496
	ds_read_b128 v[58:61], v91 offset:20736
	ds_read_b128 v[96:99], v91 offset:20800
	s_waitcnt vmcnt(4)
	v_mfma_f32_16x16x32_bf16 v[62:65], v[26:29], v[50:53], v[6:9]
	s_nop 2
	v_or_b32_e32 v6, s16, v89
	s_waitcnt lgkmcnt(1)
	v_mfma_f32_16x16x32_bf16 v[100:103], v[58:61], v[2:5], 0
	ds_read_b128 v[58:61], v91 offset:23040
	ds_read_b128 v[104:107], v91 offset:23104
	v_mul_u32_u24_e32 v8, 0x9000, v6
	v_mov_b32_e32 v7, v71
	v_mfma_f32_16x16x32_bf16 v[66:69], v[38:41], v[50:53], v[10:13]
	v_mov_b32_e32 v9, v71
	s_nop 1
	v_lshl_add_u64 v[10:11], s[4:5], 0, v[80:81]
	v_or_b32_e32 v12, 64, v6
	v_or_b32_e32 v13, 0xc0, v77
	v_lshl_add_u64 v[10:11], s[0:1], 1, v[10:11]
	v_lshlrev_b32_e32 v6, 1, v8
	v_mul_u32_u24_e32 v8, 0x9000, v12
	v_mad_u64_u32 v[12:13], s[0:1], v13, s72, v[78:79]
	v_lshl_add_u64 v[78:79], v[10:11], 0, v[6:7]
	v_lshlrev_b32_e32 v8, 1, v8
	v_lshl_add_u64 v[6:7], v[12:13], 0, v[80:81]
	v_lshl_add_u64 v[80:81], v[10:11], 0, v[8:9]
	v_lshl_add_u64 v[10:11], v[6:7], 0, s[2:3]
	s_waitcnt lgkmcnt(1)
	v_mfma_f32_16x16x32_bf16 v[108:111], v[58:61], v[2:5], 0
	ds_read_b128 v[58:61], v91 offset:25344
	ds_read_b128 v[112:115], v91 offset:25408
	global_load_dwordx4 v[6:9], v[10:11], off offset:1024
	s_nop 0
	global_load_dwordx4 v[10:13], v[10:11], off offset:1152
	v_mul_f32_e32 v38, 0x3e000000, v68
	s_waitcnt lgkmcnt(1)
	v_mfma_f32_16x16x32_bf16 v[116:119], v[58:61], v[2:5], 0
	v_mul_f32_e32 v39, 0x3e000000, v69
	s_waitcnt vmcnt(5)
	ds_write_b128 v73, v[22:25]
	s_waitcnt vmcnt(4)
	ds_write_b128 v73, v[30:33] offset:9216
	v_mfma_f32_16x16x32_bf16 v[58:61], v[42:45], v[50:53], v[14:17]
	s_waitcnt lgkmcnt(0)
	s_barrier
; #define LAS __attribute__((address_space(3)))
; template <bool LOCAL>
; __device__ __forceinline__ void na_unit(const bf16* P, const bf16* VT, bf16* YCAT, const LAS float* rpb_l, LAS bf16* buf, int b, int gr, int hp, int qblk, int tid) {
;     ...
;                 const int cc = c - NLOC;
; #pragma unroll
;                 for (int t4 = 0; t4 < 4; ++t4) {
;                     const LAS bf16* kp = cb + (16 * t4 + fr) * 72 + 8 * fq;
;                     f32x4 acc = {0.f, 0.f, 0.f, 0.f};
;                     acc = __builtin_amdgcn_mfma_f32_16x16x32_bf16(*(const LAS bf16x8*)(kp), qf[0], acc, 0, 0, 0);
;                     acc = __builtin_amdgcn_mfma_f32_16x16x32_bf16(*(const LAS bf16x8*)(kp + 32), qf[1], acc, 0, 0, 0);
; #pragma unroll
;                     for (int e = 0; e < 4; ++e) { acc[e] *= 0.125f; m = fmaxf(m, acc[e]); }
;                     sc[4 * (cc >= 0 ? cc : 0) + t4] = acc; }
;             }
;             if (sidx == NCH - 1) { m = fmaxf(m, __shfl_xor(m, 16)); m = fmaxf(m, __shfl_xor(m, 32)); }
	s_nop 0
	v_mul_f32_e32 v14, 0x3e000000, v62
	v_mul_f32_e32 v15, 0x3e000000, v63
	v_mfma_f32_16x16x32_bf16 v[54:57], v[54:57], v[50:53], v[18:21]
	s_nop 1
	v_mul_f32_e32 v40, 0x3e000000, v58
	v_mul_f32_e32 v41, 0x3e000000, v59
	v_mul_f32_e32 v77, 0x3e000000, v60
	v_mfma_f32_16x16x32_bf16 v[42:45], v[96:99], v[50:53], v[100:103]
	v_mul_f32_e32 v18, 0x3e000000, v64
	v_mul_f32_e32 v19, 0x3e000000, v65
	v_mul_f32_e32 v20, 0x3e000000, v66
	v_max3_f32 v100, v14, s75, v15
	v_mul_f32_e32 v21, 0x3e000000, v67
	v_max3_f32 v18, v100, v18, v19
	v_mfma_f32_16x16x32_bf16 v[34:37], v[34:37], v[2:5], 0
	v_max3_f32 v18, v18, v20, v21
	ds_read_b128 v[14:17], v91
	v_max3_f32 v22, v18, v38, v39
	ds_read_b128 v[18:21], v91 offset:2304
	v_mul_f32_e32 v95, 0x3e000000, v61
	v_max3_f32 v22, v22, v40, v41
	v_mul_f32_e32 v96, 0x3e000000, v54
	v_mul_f32_e32 v97, 0x3e000000, v55
	v_max3_f32 v38, v22, v77, v95
	v_mfma_f32_16x16x32_bf16 v[46:49], v[46:49], v[50:53], v[34:37]
	v_mul_f32_e32 v98, 0x3e000000, v56
	v_mul_f32_e32 v99, 0x3e000000, v57
	v_max3_f32 v38, v38, v96, v97
	ds_read_b128 v[22:25], v91 offset:64
	ds_read_b128 v[30:33], v91 offset:4608
	v_max3_f32 v38, v38, v98, v99
	ds_read_b128 v[96:99], v91 offset:2368
	v_mfma_f32_16x16x32_bf16 v[34:37], v[104:107], v[50:53], v[108:111]
	v_mul_f32_e32 v101, 0x3e000000, v46
	v_mul_f32_e32 v102, 0x3e000000, v47
	v_mul_f32_e32 v103, 0x3e000000, v48
	v_mul_f32_e32 v104, 0x3e000000, v49
	v_max3_f32 v38, v38, v101, v102
	v_mul_f32_e32 v108, 0x3e000000, v42
	v_mul_f32_e32 v109, 0x3e000000, v43
	s_waitcnt lgkmcnt(4)
	v_mfma_f32_16x16x32_bf16 v[14:17], v[14:17], v[2:5], 0
	v_max3_f32 v38, v38, v103, v104
	v_mul_f32_e32 v110, 0x3e000000, v44
	v_mul_f32_e32 v111, 0x3e000000, v45
	s_waitcnt lgkmcnt(3)
	v_mfma_f32_16x16x32_bf16 v[18:21], v[18:21], v[2:5], 0
	ds_read_b128 v[100:103], v91 offset:4672
	s_waitcnt lgkmcnt(2)
	v_mfma_f32_16x16x32_bf16 v[104:107], v[30:33], v[2:5], 0
	v_max3_f32 v30, v38, v108, v109
	v_max3_f32 v30, v30, v110, v111
	v_mfma_f32_16x16x32_bf16 v[26:29], v[112:115], v[50:53], v[116:119]
	v_mul_f32_e32 v112, 0x3e000000, v34
	v_mul_f32_e32 v113, 0x3e000000, v35
	v_mul_f32_e32 v114, 0x3e000000, v36
	v_mul_f32_e32 v115, 0x3e000000, v37
	v_max3_f32 v30, v30, v112, v113
	v_mfma_f32_16x16x32_bf16 v[38:41], v[22:25], v[50:53], v[14:17]
	s_nop 1
	v_mul_f32_e32 v116, 0x3e000000, v26
	v_mul_f32_e32 v117, 0x3e000000, v27
	v_mul_f32_e32 v118, 0x3e000000, v28
	v_max3_f32 v14, v30, v114, v115
	s_waitcnt lgkmcnt(1)
	v_mfma_f32_16x16x32_bf16 v[30:33], v[96:99], v[50:53], v[18:21]
	v_lshl_add_u64 v[248:249], v[78:79], 0, 0
	v_lshl_add_u64 v[238:239], v[80:81], 0, 0
	global_load_dwordx4 v[96:99], v[78:79], off
	global_load_dwordx4 v[108:111], v[80:81], off
	global_load_dword v250, v[248:249], off offset:128
	global_load_dword v251, v[238:239], off offset:128
	v_mul_f32_e32 v119, 0x3e000000, v29
	v_max3_f32 v14, v14, v116, v117
	v_max3_f32 v22, v14, v118, v119
	ds_read_b128 v[14:17], v91 offset:6912
	v_mul_f32_e32 v23, 0x3e000000, v38
	v_mul_f32_e32 v24, 0x3e000000, v39
	v_mul_f32_e32 v25, 0x3e000000, v40
	v_mul_f32_e32 v77, 0x3e000000, v41
	v_max3_f32 v22, v22, v23, v24
	s_waitcnt lgkmcnt(1)
	v_mfma_f32_16x16x32_bf16 v[18:21], v[100:103], v[50:53], v[104:107]
	v_mul_f32_e32 v95, 0x3e000000, v30
	v_mul_f32_e32 v100, 0x3e000000, v31
	v_max3_f32 v22, v22, v25, v77
	v_max3_f32 v77, v22, v95, v100
	ds_read_b128 v[22:25], v91 offset:6976
	s_waitcnt vmcnt(5)
	ds_write_b128 v73, v[6:9] offset:18432
	s_waitcnt vmcnt(4)
	ds_write_b128 v73, v[10:13] offset:27648
	s_waitcnt lgkmcnt(0)
	s_barrier
	ds_read_b128 v[6:9], v91 offset:18432
	v_mul_f32_e32 v101, 0x3e000000, v32
	v_mul_f32_e32 v10, 0x3e000000, v33
	v_mfma_f32_16x16x32_bf16 v[14:17], v[14:17], v[2:5], 0
	v_max3_f32 v77, v77, v101, v10
	ds_read_b128 v[10:13], v91 offset:18496
	v_mul_f32_e32 v95, 0x3e000000, v18
	v_mfma_f32_16x16x32_bf16 v[22:25], v[22:25], v[50:53], v[14:17]
	v_mul_f32_e32 v100, 0x3e000000, v21
	ds_read_b128 v[112:115], v91 offset:25408
	s_nop 1
	v_mul_f32_e32 v14, 0x3e000000, v19
	v_max3_f32 v77, v77, v95, v14
	s_waitcnt lgkmcnt(2)
	v_mfma_f32_16x16x32_bf16 v[6:9], v[6:9], v[2:5], 0
	ds_read_b128 v[14:17], v91 offset:20736
	v_mul_f32_e32 v95, 0x3e000000, v20
	v_max3_f32 v77, v77, v95, v100
	s_waitcnt lgkmcnt(2)
	v_mfma_f32_16x16x32_bf16 v[10:13], v[10:13], v[50:53], v[6:9]
	v_mul_f32_e32 v95, 0x3e000000, v22
	v_mul_f32_e32 v100, 0x3e000000, v23
	v_max3_f32 v77, v77, v95, v100
	ds_read_b128 v[6:9], v91 offset:20800
	s_waitcnt lgkmcnt(1)
	v_mfma_f32_16x16x32_bf16 v[14:17], v[14:17], v[2:5], 0
	ds_read_b128 v[100:103], v91 offset:23040
	v_mul_f32_e32 v95, 0x3e000000, v24
	v_mul_f32_e32 v104, 0x3e000000, v25
	s_waitcnt lgkmcnt(1)
	v_mfma_f32_16x16x32_bf16 v[14:17], v[6:9], v[50:53], v[14:17]
	ds_read_b128 v[6:9], v91 offset:23104
	v_max3_f32 v77, v77, v95, v104
	ds_read_b128 v[104:107], v91 offset:25344
	s_waitcnt lgkmcnt(2)
	v_mfma_f32_16x16x32_bf16 v[100:103], v[100:103], v[2:5], 0
	v_mul_f32_e32 v95, 0x3e000000, v10
	v_mul_f32_e32 v116, 0x3e000000, v11
	v_mul_f32_e32 v117, 0x3e000000, v12
	s_waitcnt lgkmcnt(1)
	v_mfma_f32_16x16x32_bf16 v[6:9], v[6:9], v[50:53], v[100:103]
	v_mul_f32_e32 v118, 0x3e000000, v13
	v_max3_f32 v77, v77, v95, v116
	v_mul_f32_e32 v119, 0x3e000000, v14
	v_mul_f32_e32 v120, 0x3e000000, v15
	s_waitcnt lgkmcnt(0)
	v_mfma_f32_16x16x32_bf16 v[2:5], v[104:107], v[2:5], 0
	v_max3_f32 v77, v77, v117, v118
	v_mul_f32_e32 v91, 0x3e000000, v16
	v_mul_f32_e32 v100, 0x3e000000, v17
	v_max3_f32 v77, v77, v119, v120
	v_mul_f32_e32 v101, 0x3e000000, v6
	v_mul_f32_e32 v102, 0x3e000000, v7
	v_max3_f32 v77, v77, v91, v100
	v_mul_f32_e32 v103, 0x3e000000, v8
	v_mul_f32_e32 v104, 0x3e000000, v9
	v_max3_f32 v77, v77, v101, v102
	v_mfma_f32_16x16x32_bf16 v[2:5], v[112:115], v[50:53], v[2:5]
	v_max3_f32 v77, v77, v103, v104
	v_lshl_add_u64 v[248:249], v[78:79], 0, 0
	v_lshl_add_u64 v[238:239], v[80:81], 0, 0
	global_load_dwordx4 v[100:103], v[78:79], off offset:128
	global_load_dwordx4 v[104:107], v[80:81], off offset:128
	global_load_dword v250, v[248:249], off offset:256
	global_load_dword v251, v[238:239], off offset:256
	s_waitcnt vmcnt(7)
	ds_write_b128 v73, v[96:99]
	s_waitcnt vmcnt(6)
	ds_write_b128 v73, v[108:111] offset:9216
	s_nop 0
	v_mul_f32_e32 v50, 0x3e000000, v2
	v_mul_f32_e32 v51, 0x3e000000, v3
	v_mul_f32_e32 v52, 0x3e000000, v4
	v_mul_f32_e32 v53, 0x3e000000, v5
	v_max3_f32 v50, v77, v50, v51
	v_max3_f32 v51, v50, v52, v53
	v_cndmask_b32_e32 v50, v83, v84, vcc
	v_lshlrev_b32_e32 v50, 2, v50
	ds_bpermute_b32 v52, v50, v51
	v_cmp_lt_i32_e32 vcc, v86, v85
	s_waitcnt lgkmcnt(0)
	s_barrier
; #define LAS __attribute__((address_space(3)))
; __device__ __forceinline__ unsigned cvt_pk_bf16(float lo, float hi) { const float __attribute__((ext_vector_type(2))) v = {lo, hi}; return __builtin_bit_cast(unsigned, __builtin_convertvector(v, bf16x2_t)); }
; template <bool LOCAL>
; __device__ __forceinline__ void na_unit(const bf16* P, const bf16* VT, bf16* YCAT, const LAS float* rpb_l, LAS bf16* buf, int b, int gr, int hp, int qblk, int tid) {
;     ...
;             if (sidx == NCH - 1) { m = fmaxf(m, __shfl_xor(m, 16)); m = fmaxf(m, __shfl_xor(m, 32)); }
;     ...
;             } else {
;                 const int cc = c - NLOC;
; #pragma unroll
;                 for (int p2 = 0; p2 < 2; ++p2) {
;                     float p[8];
; #pragma unroll
;                     for (int e = 0; e < 4; ++e) { p[e] = __expf(sc[4 * (cc >= 0 ? cc : 0) + 2 * p2][e] - m); p[4 + e] = __expf(sc[4 * (cc >= 0 ? cc : 0) + 2 * p2 + 1][e] - m); }
; #pragma unroll
;                     for (int e = 0; e < 8; ++e) lsum += p[e];
;                     const bf16x8 pf = __builtin_bit_cast(bf16x8, (v4u){pg8::cvt_pk_bf16(p[0], p[1]), pg8::cvt_pk_bf16(p[2], p[3]), pg8::cvt_pk_bf16(p[4], p[5]), pg8::cvt_pk_bf16(p[6], p[7])});
; #pragma unroll
;                     for (int dt = 0; dt < 4; ++dt) { const LAS bf16* vp = cb + (16 * dt + fr) * 72 + 32 * p2 + 4 * fq;
;                         o[dt] = __builtin_amdgcn_mfma_f32_16x16x32_bf16(frag44(vp, vp + 16), pf, o[dt], 0, 0, 0); }
;                 }
	v_max_f32_e32 v52, v52, v52
	v_max_f32_e32 v52, v51, v52
	v_cndmask_b32_e32 v51, v83, v86, vcc
	v_lshlrev_b32_e32 v51, 2, v51
	ds_bpermute_b32 v53, v51, v52
	s_waitcnt lgkmcnt(0)
	v_max_f32_e32 v53, v53, v53
	v_max_f32_e32 v77, v52, v53
	v_fma_f32 v52, v62, s74, -v77
	v_fma_f32 v64, v64, s74, -v77
	v_mul_f32_e32 v52, 0x3fb8aa3b, v52
	v_fma_f32 v62, v63, s74, -v77
	v_mul_f32_e32 v64, 0x3fb8aa3b, v64
	v_fma_f32 v65, v65, s74, -v77
	v_exp_f32_e32 v53, v52
	v_fma_f32 v52, v66, s74, -v77
	v_mul_f32_e32 v62, 0x3fb8aa3b, v62
	v_exp_f32_e32 v66, v64
	v_fma_f32 v64, v68, s74, -v77
	v_mul_f32_e32 v65, 0x3fb8aa3b, v65
	v_add3_u32 v68, v87, v76, v88
	v_exp_f32_e32 v63, v62
	v_fma_f32 v62, v67, s74, -v77
	v_exp_f32_e32 v67, v65
	v_fma_f32 v65, v69, s74, -v77
	v_add_u32_e32 v69, 0x800, v68
	v_add_u32_e32 v91, 0x1000, v68
	v_add_u32_e32 v95, 0x1800, v68
	ds_read2_b64 v[96:99], v68 offset1:4
	ds_read2_b64 v[112:115], v69 offset0:32 offset1:36
	ds_read2_b64 v[116:119], v91 offset0:64 offset1:68
	ds_read2_b64 v[120:123], v95 offset0:96 offset1:100
	v_mul_f32_e32 v52, 0x3fb8aa3b, v52
	v_mul_f32_e32 v62, 0x3fb8aa3b, v62
	v_mul_f32_e32 v64, 0x3fb8aa3b, v64
	v_mul_f32_e32 v65, 0x3fb8aa3b, v65
	v_exp_f32_e32 v52, v52
	v_exp_f32_e32 v62, v62
	v_exp_f32_e32 v64, v64
	v_exp_f32_e32 v65, v65
	v_cvt_pk_bf16_f32 v108, v53, v63
	v_cvt_pk_bf16_f32 v109, v66, v67
	v_cvt_pk_bf16_f32 v110, v52, v62
	v_cvt_pk_bf16_f32 v111, v64, v65
	v_fma_f32 v58, v58, s74, -v77
	v_fma_f32 v54, v54, s74, -v77
	s_waitcnt lgkmcnt(3)
	v_mfma_f32_16x16x32_bf16 v[96:99], v[96:99], v[108:111], 0
	v_fma_f32 v59, v59, s74, -v77
	v_fma_f32 v55, v55, s74, -v77
	v_fma_f32 v60, v60, s74, -v77
	s_waitcnt lgkmcnt(2)
	v_mfma_f32_16x16x32_bf16 v[112:115], v[112:115], v[108:111], 0
	v_fma_f32 v56, v56, s74, -v77
	v_fma_f32 v61, v61, s74, -v77
	v_fma_f32 v57, v57, s74, -v77
	s_waitcnt lgkmcnt(1)
	v_mfma_f32_16x16x32_bf16 v[116:119], v[116:119], v[108:111], 0
	v_mul_f32_e32 v58, 0x3fb8aa3b, v58
	v_mul_f32_e32 v54, 0x3fb8aa3b, v54
	v_mul_f32_e32 v59, 0x3fb8aa3b, v59
	s_waitcnt lgkmcnt(0)
	v_mfma_f32_16x16x32_bf16 v[108:111], v[120:123], v[108:111], 0
	ds_read2_b64 v[120:123], v68 offset0:8 offset1:12
	v_mul_f32_e32 v55, 0x3fb8aa3b, v55
	v_mul_f32_e32 v60, 0x3fb8aa3b, v60
	v_mul_f32_e32 v56, 0x3fb8aa3b, v56
	v_mul_f32_e32 v61, 0x3fb8aa3b, v61
	v_mul_f32_e32 v57, 0x3fb8aa3b, v57
	v_exp_f32_e32 v58, v58
	v_exp_f32_e32 v54, v54
	v_exp_f32_e32 v59, v59
	v_exp_f32_e32 v55, v55
	v_exp_f32_e32 v60, v60
	v_exp_f32_e32 v56, v56
	v_exp_f32_e32 v61, v61
	v_exp_f32_e32 v57, v57
	v_cvt_pk_bf16_f32 v124, v58, v59
	v_cvt_pk_bf16_f32 v126, v54, v55
	v_cvt_pk_bf16_f32 v125, v60, v61
	v_cvt_pk_bf16_f32 v127, v56, v57
	v_fma_f32 v42, v42, s74, -v77
	v_mul_f32_e32 v42, 0x3fb8aa3b, v42
	s_waitcnt lgkmcnt(0)
	v_mfma_f32_16x16x32_bf16 v[96:99], v[120:123], v[124:127], v[96:99]
	ds_read2_b64 v[120:123], v69 offset0:40 offset1:44
	v_fma_f32 v46, v46, s74, -v77
	v_mul_f32_e32 v46, 0x3fb8aa3b, v46
	s_waitcnt lgkmcnt(0)
	v_mfma_f32_16x16x32_bf16 v[112:115], v[120:123], v[124:127], v[112:115]
	ds_read2_b64 v[120:123], v91 offset0:72 offset1:76
	v_add_u32_e32 v137, 0x5000, v68
	v_fma_f32 v26, v26, s74, -v77
	s_waitcnt lgkmcnt(0)
	v_mfma_f32_16x16x32_bf16 v[116:119], v[120:123], v[124:127], v[116:119]
	ds_read2_b64 v[120:123], v95 offset0:104 offset1:108
	v_lshl_add_u64 v[248:249], v[78:79], 0, 0
	v_lshl_add_u64 v[238:239], v[80:81], 0, 0
	global_load_dwordx4 v[128:131], v[78:79], off offset:256
	global_load_dwordx4 v[132:135], v[80:81], off offset:256
	global_load_dword v250, v[248:249], off offset:384
	global_load_dword v251, v[238:239], off offset:384
	s_waitcnt vmcnt(7)
	ds_write_b128 v73, v[100:103] offset:18432
	s_waitcnt vmcnt(6)
	ds_write_b128 v73, v[104:107] offset:27648
	s_waitcnt lgkmcnt(2)
	v_mfma_f32_16x16x32_bf16 v[108:111], v[120:123], v[124:127], v[108:111]
	v_exp_f32_e32 v121, v42
	v_fma_f32 v42, v47, s74, -v77
	v_mul_f32_e32 v42, 0x3fb8aa3b, v42
	v_exp_f32_e32 v122, v42
	v_fma_f32 v42, v43, s74, -v77
	v_mul_f32_e32 v42, 0x3fb8aa3b, v42
	v_exp_f32_e32 v123, v42
	v_fma_f32 v42, v48, s74, -v77
	v_mul_f32_e32 v42, 0x3fb8aa3b, v42
	v_exp_f32_e32 v124, v42
	v_fma_f32 v42, v44, s74, -v77
	v_mul_f32_e32 v42, 0x3fb8aa3b, v42
	v_add_u32_e32 v126, 0x4800, v68
	s_waitcnt lgkmcnt(0)
	s_barrier
; #define LAS __attribute__((address_space(3)))
; __device__ __forceinline__ unsigned cvt_pk_bf16(float lo, float hi) { const float __attribute__((ext_vector_type(2))) v = {lo, hi}; return __builtin_bit_cast(unsigned, __builtin_convertvector(v, bf16x2_t)); }
; template <bool LOCAL>
; __device__ __forceinline__ void na_unit(const bf16* P, const bf16* VT, bf16* YCAT, const LAS float* rpb_l, LAS bf16* buf, int b, int gr, int hp, int qblk, int tid) {
;     ...
;             } else {
;                 const int cc = c - NLOC;
; #pragma unroll
;                 for (int p2 = 0; p2 < 2; ++p2) {
;                     float p[8];
; #pragma unroll
;                     for (int e = 0; e < 4; ++e) { p[e] = __expf(sc[4 * (cc >= 0 ? cc : 0) + 2 * p2][e] - m); p[4 + e] = __expf(sc[4 * (cc >= 0 ? cc : 0) + 2 * p2 + 1][e] - m); }
; #pragma unroll
;                     for (int e = 0; e < 8; ++e) lsum += p[e];
;                     const bf16x8 pf = __builtin_bit_cast(bf16x8, (v4u){pg8::cvt_pk_bf16(p[0], p[1]), pg8::cvt_pk_bf16(p[2], p[3]), pg8::cvt_pk_bf16(p[4], p[5]), pg8::cvt_pk_bf16(p[6], p[7])});
; #pragma unroll
;                     for (int dt = 0; dt < 4; ++dt) { const LAS bf16* vp = cb + (16 * dt + fr) * 72 + 32 * p2 + 4 * fq;
;                         o[dt] = __builtin_amdgcn_mfma_f32_16x16x32_bf16(frag44(vp, vp + 16), pf, o[dt], 0, 0, 0); }
;                 }
	v_exp_f32_e32 v120, v46
	v_exp_f32_e32 v125, v42
	v_fma_f32 v42, v49, s74, -v77
	ds_read2_b64 v[46:49], v126 offset1:4
	v_mul_f32_e32 v42, 0x3fb8aa3b, v42
	v_exp_f32_e32 v127, v42
	v_fma_f32 v42, v45, s74, -v77
	v_mul_f32_e32 v42, 0x3fb8aa3b, v42
	v_exp_f32_e32 v136, v42
	v_cvt_pk_bf16_f32 v42, v120, v122
	v_cvt_pk_bf16_f32 v43, v124, v127
	v_cvt_pk_bf16_f32 v44, v121, v123
	v_cvt_pk_bf16_f32 v45, v125, v136
	v_mul_f32_e32 v26, 0x3fb8aa3b, v26
	v_fma_f32 v34, v34, s74, -v77
	s_waitcnt lgkmcnt(0)
	v_mfma_f32_16x16x32_bf16 v[46:49], v[46:49], v[42:45], v[96:99]
	v_mul_f32_e32 v34, 0x3fb8aa3b, v34
	v_fma_f32 v30, v30, s74, -v77
	v_mul_f32_e32 v30, 0x3fb8aa3b, v30
	ds_read2_b64 v[96:99], v137 offset0:32 offset1:36
	s_waitcnt lgkmcnt(0)
	v_mfma_f32_16x16x32_bf16 v[96:99], v[96:99], v[42:45], v[112:115]
	s_nop 2
	v_add_u32_e32 v112, 0x5800, v68
	v_add_u32_e32 v113, 0x6000, v68
	ds_read2_b64 v[100:103], v112 offset0:64 offset1:68
	ds_read2_b64 v[104:107], v113 offset0:96 offset1:100
	s_waitcnt lgkmcnt(1)
	v_mfma_f32_16x16x32_bf16 v[100:103], v[100:103], v[42:45], v[116:119]
	v_fma_f32 v38, v38, s74, -v77
	v_mul_f32_e32 v38, 0x3fb8aa3b, v38
	v_fma_f32 v18, v18, s74, -v77
	s_waitcnt lgkmcnt(0)
	v_mfma_f32_16x16x32_bf16 v[42:45], v[104:107], v[42:45], v[108:111]
	v_mul_f32_e32 v18, 0x3fb8aa3b, v18
	v_fma_f32 v10, v10, s74, -v77
	v_mul_f32_e32 v10, 0x3fb8aa3b, v10
	v_exp_f32_e32 v109, v26
	v_fma_f32 v26, v35, s74, -v77
	v_mul_f32_e32 v26, 0x3fb8aa3b, v26
	v_exp_f32_e32 v110, v26
	v_fma_f32 v26, v27, s74, -v77
	v_mul_f32_e32 v26, 0x3fb8aa3b, v26
	v_exp_f32_e32 v111, v26
	v_fma_f32 v26, v36, s74, -v77
	v_mul_f32_e32 v26, 0x3fb8aa3b, v26
	v_exp_f32_e32 v114, v26
	v_fma_f32 v26, v28, s74, -v77
	v_mul_f32_e32 v26, 0x3fb8aa3b, v26
	v_exp_f32_e32 v108, v34
	v_exp_f32_e32 v115, v26
	v_fma_f32 v26, v37, s74, -v77
	ds_read2_b64 v[34:37], v126 offset0:8 offset1:12
	v_mul_f32_e32 v26, 0x3fb8aa3b, v26
	v_exp_f32_e32 v116, v26
	v_fma_f32 v26, v29, s74, -v77
	v_mul_f32_e32 v26, 0x3fb8aa3b, v26
	v_exp_f32_e32 v117, v26
	v_cvt_pk_bf16_f32 v26, v108, v110
	v_cvt_pk_bf16_f32 v27, v114, v116
	v_cvt_pk_bf16_f32 v28, v109, v111
	v_cvt_pk_bf16_f32 v29, v115, v117
	v_fma_f32 v2, v2, s74, -v77
	v_mul_f32_e32 v2, 0x3fb8aa3b, v2
	s_waitcnt lgkmcnt(0)
	v_mfma_f32_16x16x32_bf16 v[34:37], v[34:37], v[26:29], v[46:49]
	v_fma_f32 v6, v6, s74, -v77
	v_mul_f32_e32 v6, 0x3fb8aa3b, v6
	s_nop 0
	ds_read2_b64 v[46:49], v137 offset0:40 offset1:44
	s_waitcnt lgkmcnt(0)
	v_mfma_f32_16x16x32_bf16 v[46:49], v[46:49], v[26:29], v[96:99]
	s_nop 2
	ds_read2_b64 v[96:99], v112 offset0:72 offset1:76
	s_waitcnt lgkmcnt(0)
	v_mfma_f32_16x16x32_bf16 v[96:99], v[96:99], v[26:29], v[100:103]
	s_nop 2
	ds_read2_b64 v[100:103], v113 offset0:104 offset1:108
	global_load_dwordx4 v[104:107], v[78:79], off offset:384
	s_nop 0
	global_load_dwordx4 v[78:81], v[80:81], off offset:384
	s_waitcnt vmcnt(5)
	ds_write_b128 v73, v[128:131]
	s_waitcnt vmcnt(4)
	ds_write_b128 v73, v[132:135] offset:9216
	s_waitcnt lgkmcnt(2)
	v_mfma_f32_16x16x32_bf16 v[26:29], v[100:103], v[26:29], v[42:45]
	v_exp_f32_e32 v101, v30
	v_fma_f32 v30, v39, s74, -v77
	v_mul_f32_e32 v30, 0x3fb8aa3b, v30
	v_exp_f32_e32 v102, v30
	v_fma_f32 v30, v31, s74, -v77
	v_mul_f32_e32 v30, 0x3fb8aa3b, v30
	v_exp_f32_e32 v103, v30
	v_fma_f32 v30, v40, s74, -v77
	v_mul_f32_e32 v30, 0x3fb8aa3b, v30
	v_exp_f32_e32 v118, v30
	v_fma_f32 v30, v32, s74, -v77
	v_mul_f32_e32 v30, 0x3fb8aa3b, v30
	s_waitcnt lgkmcnt(0)
	s_barrier
	v_exp_f32_e32 v100, v38
	v_exp_f32_e32 v119, v30
	v_fma_f32 v30, v41, s74, -v77
	ds_read2_b64 v[38:41], v68 offset1:4
	v_mul_f32_e32 v30, 0x3fb8aa3b, v30
	v_exp_f32_e32 v128, v30
	v_fma_f32 v30, v33, s74, -v77
	v_mul_f32_e32 v30, 0x3fb8aa3b, v30
	v_exp_f32_e32 v129, v30
	v_cvt_pk_bf16_f32 v30, v100, v102
	v_cvt_pk_bf16_f32 v31, v118, v128
	v_cvt_pk_bf16_f32 v32, v101, v103
	v_cvt_pk_bf16_f32 v33, v119, v129
	ds_read2_b64 v[42:45], v91 offset0:64 offset1:68
	s_waitcnt lgkmcnt(1)
	v_mfma_f32_16x16x32_bf16 v[34:37], v[38:41], v[30:33], v[34:37]
	ds_read2_b64 v[38:41], v69 offset0:32 offset1:36
	s_waitcnt lgkmcnt(0)
	v_mfma_f32_16x16x32_bf16 v[38:41], v[38:41], v[30:33], v[46:49]
	s_nop 2
	ds_read2_b64 v[46:49], v95 offset0:96 offset1:100
	s_waitcnt lgkmcnt(0)
	v_mfma_f32_16x16x32_bf16 v[26:29], v[46:49], v[30:33], v[26:29]
	v_exp_f32_e32 v46, v18
	v_fma_f32 v18, v22, s74, -v77
	v_mul_f32_e32 v18, 0x3fb8aa3b, v18
	v_exp_f32_e32 v47, v18
	v_fma_f32 v18, v19, s74, -v77
	v_mul_f32_e32 v18, 0x3fb8aa3b, v18
	v_exp_f32_e32 v48, v18
	v_fma_f32 v18, v23, s74, -v77
	v_mul_f32_e32 v18, 0x3fb8aa3b, v18
	v_exp_f32_e32 v49, v18
	v_fma_f32 v18, v20, s74, -v77
	v_mul_f32_e32 v18, 0x3fb8aa3b, v18
	v_mfma_f32_16x16x32_bf16 v[42:45], v[42:45], v[30:33], v[96:99]
	ds_read2_b64 v[30:33], v69 offset0:40 offset1:44
	s_nop 1
	v_exp_f32_e32 v96, v18
	v_fma_f32 v18, v24, s74, -v77
	v_mul_f32_e32 v18, 0x3fb8aa3b, v18
	v_exp_f32_e32 v97, v18
	v_fma_f32 v18, v21, s74, -v77
	v_mul_f32_e32 v22, 0x3fb8aa3b, v18
	ds_read2_b64 v[18:21], v68 offset0:8 offset1:12
	v_exp_f32_e32 v68, v22
	v_fma_f32 v22, v25, s74, -v77
	v_mul_f32_e32 v22, 0x3fb8aa3b, v22
	v_exp_f32_e32 v98, v22
	v_cvt_pk_bf16_f32 v22, v46, v48
	v_cvt_pk_bf16_f32 v23, v96, v68
	v_cvt_pk_bf16_f32 v24, v47, v49
	v_cvt_pk_bf16_f32 v25, v97, v98
	s_waitcnt lgkmcnt(0)
	s_nop 0
	v_mfma_f32_16x16x32_bf16 v[18:21], v[18:21], v[22:25], v[34:37]
	v_mfma_f32_16x16x32_bf16 v[30:33], v[30:33], v[22:25], v[38:41]
	s_nop 1
	ds_read2_b64 v[34:37], v91 offset0:72 offset1:76
	ds_read2_b64 v[38:41], v95 offset0:104 offset1:108
	s_waitcnt lgkmcnt(1)
	v_mfma_f32_16x16x32_bf16 v[34:37], v[34:37], v[22:25], v[42:45]
	s_waitcnt vmcnt(1)
	ds_write_b128 v73, v[104:107] offset:18432
	s_waitcnt vmcnt(0)
	ds_write_b128 v73, v[78:81] offset:27648
	s_waitcnt lgkmcnt(0)
	s_barrier
; #define LAS __attribute__((address_space(3)))
; __device__ __forceinline__ unsigned cvt_pk_bf16(float lo, float hi) { const float __attribute__((ext_vector_type(2))) v = {lo, hi}; return __builtin_bit_cast(unsigned, __builtin_convertvector(v, bf16x2_t)); }
; #define NA_STORE(sidx) do { LAS bf16* d_ = buf + ((sidx) & 1) * 9216; _Pragma("unroll") for (int q_ = 0; q_ < 2; ++q_) *(LAS v4u*)(d_ + q_ * 4608 + lrow * 72 + lseg * 8) = ld[(sidx) & 1][q_]; } while (0)
; template <bool LOCAL>
; __device__ __forceinline__ void na_unit(const bf16* P, const bf16* VT, bf16* YCAT, const LAS float* rpb_l, LAS bf16* buf, int b, int gr, int hp, int qblk, int tid) {
;     ...
;                     for (int e = 0; e < 4; ++e) { p[e] = __expf(sc[4 * (cc >= 0 ? cc : 0) + 2 * p2][e] - m); p[4 + e] = __expf(sc[4 * (cc >= 0 ? cc : 0) + 2 * p2 + 1][e] - m); }
; #pragma unroll
;                     for (int e = 0; e < 8; ++e) lsum += p[e];
;                     const bf16x8 pf = __builtin_bit_cast(bf16x8, (v4u){pg8::cvt_pk_bf16(p[0], p[1]), pg8::cvt_pk_bf16(p[2], p[3]), pg8::cvt_pk_bf16(p[4], p[5]), pg8::cvt_pk_bf16(p[6], p[7])});
; #pragma unroll
;                     for (int dt = 0; dt < 4; ++dt) { const LAS bf16* vp = cb + (16 * dt + fr) * 72 + 32 * p2 + 4 * fq;
;                         o[dt] = __builtin_amdgcn_mfma_f32_16x16x32_bf16(frag44(vp, vp + 16), pf, o[dt], 0, 0, 0); }
;                 }
;             }
;         }
;         if (sidx + 1 < 2 * NCH) NA_STORE(sidx + 1);
;         __syncthreads();
;     }
;     ...
;     lsum += __shfl_xor(lsum, 16); lsum += __shfl_xor(lsum, 32);
;     const float inv = 1.f / lsum;
;     bf16* op = YCAT + (size_t)(qrow0 + fr) * D + 512 + h * 64 + 4 * fq;
; #pragma unroll
;     for (int dt = 0; dt < 4; ++dt) { v2u w; w.x = pg8::cvt_pk_bf16(o[dt][0] * inv, o[dt][1] * inv); w.y = pg8::cvt_pk_bf16(o[dt][2] * inv, o[dt][3] * inv); *(v2u*)(op + dt * 16) = w; }
	v_mfma_f32_16x16x32_bf16 v[22:25], v[38:41], v[22:25], v[26:29]
	v_exp_f32_e32 v38, v10
	v_fma_f32 v10, v14, s74, -v77
	v_mul_f32_e32 v10, 0x3fb8aa3b, v10
	v_exp_f32_e32 v39, v10
	v_fma_f32 v10, v11, s74, -v77
	v_mul_f32_e32 v10, 0x3fb8aa3b, v10
	v_exp_f32_e32 v40, v10
	v_fma_f32 v10, v15, s74, -v77
	v_mul_f32_e32 v10, 0x3fb8aa3b, v10
	v_exp_f32_e32 v41, v10
	v_fma_f32 v10, v12, s74, -v77
	v_mul_f32_e32 v10, 0x3fb8aa3b, v10
	v_exp_f32_e32 v42, v10
	v_fma_f32 v10, v16, s74, -v77
	v_mul_f32_e32 v10, 0x3fb8aa3b, v10
	v_exp_f32_e32 v43, v10
	v_fma_f32 v10, v13, s74, -v77
	ds_read2_b64 v[26:29], v112 offset0:64 offset1:68
	v_mul_f32_e32 v14, 0x3fb8aa3b, v10
	v_exp_f32_e32 v44, v14
	v_fma_f32 v14, v17, s74, -v77
	v_mul_f32_e32 v14, 0x3fb8aa3b, v14
	v_exp_f32_e32 v45, v14
	v_cvt_pk_bf16_f32 v14, v38, v40
	v_cvt_pk_bf16_f32 v15, v42, v44
	v_cvt_pk_bf16_f32 v16, v39, v41
	v_cvt_pk_bf16_f32 v17, v43, v45
	ds_read2_b64 v[10:13], v126 offset1:4
	v_mov_b32_e32 v73, v71
	s_waitcnt lgkmcnt(1)
	v_mfma_f32_16x16x32_bf16 v[26:29], v[26:29], v[14:17], v[34:37]
	s_nop 2
	v_add_f32_e32 v34, 0, v53
	v_add_f32_e32 v34, v63, v34
	v_add_f32_e32 v34, v66, v34
	v_add_f32_e32 v34, v67, v34
	v_add_f32_e32 v34, v52, v34
	v_add_f32_e32 v34, v62, v34
	v_add_f32_e32 v34, v64, v34
	v_add_f32_e32 v34, v65, v34
	v_add_f32_e32 v34, v58, v34
	v_add_f32_e32 v34, v59, v34
	v_add_f32_e32 v34, v60, v34
	v_add_f32_e32 v34, v61, v34
	v_add_f32_e32 v34, v54, v34
	v_add_f32_e32 v34, v55, v34
	v_add_f32_e32 v34, v56, v34
	v_add_f32_e32 v34, v57, v34
	s_waitcnt lgkmcnt(0)
	v_mfma_f32_16x16x32_bf16 v[10:13], v[10:13], v[14:17], v[18:21]
	v_add_f32_e32 v34, v120, v34
	v_add_f32_e32 v34, v122, v34
	v_add_f32_e32 v34, v124, v34
	ds_read2_b64 v[18:21], v137 offset0:32 offset1:36
	v_add_f32_e32 v34, v127, v34
	v_add_f32_e32 v34, v121, v34
	v_add_f32_e32 v34, v123, v34
	v_add_f32_e32 v34, v125, v34
	v_add_f32_e32 v34, v136, v34
	v_add_f32_e32 v34, v108, v34
	s_waitcnt lgkmcnt(0)
	v_mfma_f32_16x16x32_bf16 v[18:21], v[18:21], v[14:17], v[30:33]
	v_add_f32_e32 v34, v110, v34
	s_nop 1
	ds_read2_b64 v[30:33], v113 offset0:96 offset1:100
	v_add_f32_e32 v34, v114, v34
	v_add_f32_e32 v34, v116, v34
	v_add_f32_e32 v34, v109, v34
	v_add_f32_e32 v34, v111, v34
	v_add_f32_e32 v34, v115, v34
	v_add_f32_e32 v34, v117, v34
	v_add_f32_e32 v34, v100, v34
	v_add_f32_e32 v34, v102, v34
	s_waitcnt lgkmcnt(0)
	v_mfma_f32_16x16x32_bf16 v[14:17], v[30:33], v[14:17], v[22:25]
	v_add_f32_e32 v34, v118, v34
	v_add_f32_e32 v34, v128, v34
	v_add_f32_e32 v34, v101, v34
	v_exp_f32_e32 v23, v2
	v_fma_f32 v2, v7, s74, -v77
	v_mul_f32_e32 v2, 0x3fb8aa3b, v2
	v_exp_f32_e32 v24, v2
	v_fma_f32 v2, v3, s74, -v77
	v_mul_f32_e32 v2, 0x3fb8aa3b, v2
	v_add_f32_e32 v34, v103, v34
	v_exp_f32_e32 v25, v2
	v_fma_f32 v2, v8, s74, -v77
	v_add_f32_e32 v34, v119, v34
	v_mul_f32_e32 v2, 0x3fb8aa3b, v2
	v_add_f32_e32 v34, v129, v34
	v_exp_f32_e32 v30, v2
	v_fma_f32 v2, v4, s74, -v77
	v_add_f32_e32 v34, v46, v34
	v_mul_f32_e32 v2, 0x3fb8aa3b, v2
	v_add_f32_e32 v34, v48, v34
	v_exp_f32_e32 v22, v6
	v_exp_f32_e32 v31, v2
	v_fma_f32 v2, v9, s74, -v77
	ds_read2_b64 v[6:9], v126 offset0:8 offset1:12
	v_add_f32_e32 v34, v96, v34
	v_mul_f32_e32 v2, 0x3fb8aa3b, v2
	v_add_f32_e32 v34, v68, v34
	v_exp_f32_e32 v32, v2
	v_fma_f32 v2, v5, s74, -v77
	v_add_f32_e32 v34, v47, v34
	v_mul_f32_e32 v2, 0x3fb8aa3b, v2
	v_add_f32_e32 v34, v49, v34
	v_exp_f32_e32 v33, v2
	v_add_f32_e32 v34, v97, v34
	v_add_f32_e32 v34, v98, v34
	v_add_f32_e32 v34, v38, v34
	v_add_f32_e32 v34, v40, v34
	v_cvt_pk_bf16_f32 v2, v22, v24
	v_cvt_pk_bf16_f32 v3, v30, v32
	v_cvt_pk_bf16_f32 v4, v23, v25
	v_cvt_pk_bf16_f32 v5, v31, v33
	v_add_f32_e32 v34, v42, v34
	v_add_f32_e32 v34, v44, v34
	s_waitcnt lgkmcnt(0)
	v_mfma_f32_16x16x32_bf16 v[6:9], v[6:9], v[2:5], v[10:13]
	v_add_f32_e32 v34, v39, v34
	v_add_f32_e32 v34, v41, v34
	v_add_f32_e32 v34, v43, v34
	ds_read2_b64 v[10:13], v137 offset0:40 offset1:44
	v_add_f32_e32 v34, v45, v34
	v_add_f32_e32 v22, v22, v34
	v_add_f32_e32 v22, v24, v22
	v_add_f32_e32 v22, v30, v22
	v_add_f32_e32 v22, v32, v22
	s_waitcnt lgkmcnt(0)
	v_mfma_f32_16x16x32_bf16 v[10:13], v[10:13], v[2:5], v[18:21]
	s_nop 2
	ds_read2_b64 v[18:21], v112 offset0:72 offset1:76
	v_add_f32_e32 v22, v23, v22
	v_add_f32_e32 v22, v25, v22
	v_add_f32_e32 v22, v31, v22
	v_add_f32_e32 v30, v33, v22
	ds_bpermute_b32 v31, v50, v30
	ds_read2_b64 v[22:25], v113 offset0:104 offset1:108
	s_waitcnt lgkmcnt(2)
	v_mfma_f32_16x16x32_bf16 v[18:21], v[18:21], v[2:5], v[26:29]
	v_mov_b32_e32 v77, v71
	s_waitcnt lgkmcnt(1)
	s_nop 0
	v_add_f32_e32 v26, v30, v31
	ds_bpermute_b32 v27, v51, v26
	s_waitcnt lgkmcnt(1)
	v_mfma_f32_16x16x32_bf16 v[14:17], v[22:25], v[2:5], v[14:17]
	s_waitcnt lgkmcnt(0)
	v_add_f32_e32 v2, v26, v27
	v_div_scale_f32 v3, s[0:1], v2, v2, 1.0
	v_rcp_f32_e32 v4, v3
	s_barrier
	s_mov_b64 s[0:1], 0
	v_fma_f32 v5, -v3, v4, 1.0
	v_fmac_f32_e32 v4, v5, v4
	v_div_scale_f32 v5, vcc, 1.0, v2, 1.0
	v_mul_f32_e32 v22, v5, v4
	v_fma_f32 v23, -v3, v22, v5
	v_fmac_f32_e32 v22, v23, v4
	v_fma_f32 v3, -v3, v22, v5
	v_div_fmas_f32 v3, v3, v4, v22
	v_div_fixup_f32 v22, v3, v2, 1.0
	v_lshlrev_b64 v[2:3], 11, v[72:73]
	v_lshl_add_u64 v[2:3], s[10:11], 0, v[2:3]
	v_lshl_add_u64 v[2:3], v[2:3], 0, v[74:75]
	v_pk_mul_f32 v[6:7], v[6:7], v[22:23] op_sel_hi:[1,0]
	v_pk_mul_f32 v[8:9], v[8:9], v[22:23] op_sel_hi:[1,0]
	v_lshl_add_u64 v[4:5], v[2:3], 0, v[76:77]
	v_cvt_pk_bf16_f32 v6, v6, v7
	v_cvt_pk_bf16_f32 v7, v8, v9
	global_store_dwordx2 v[4:5], v[6:7], off offset:1024
	v_pk_mul_f32 v[6:7], v[10:11], v[22:23] op_sel_hi:[1,0]
	v_pk_mul_f32 v[8:9], v[12:13], v[22:23] op_sel_hi:[1,0]
	v_cvt_pk_bf16_f32 v6, v6, v7
	v_cvt_pk_bf16_f32 v7, v8, v9
	global_store_dwordx2 v[4:5], v[6:7], off offset:1056
	v_pk_mul_f32 v[6:7], v[18:19], v[22:23] op_sel_hi:[1,0]
	v_pk_mul_f32 v[8:9], v[20:21], v[22:23] op_sel_hi:[1,0]
	v_cvt_pk_bf16_f32 v6, v6, v7
	v_cvt_pk_bf16_f32 v7, v8, v9
	v_lshl_add_u64 v[2:3], v[4:5], 0, s[12:13]
	global_store_dwordx2 v[4:5], v[6:7], off offset:1088
	v_pk_mul_f32 v[4:5], v[14:15], v[22:23] op_sel_hi:[1,0]
	v_pk_mul_f32 v[6:7], v[16:17], v[22:23] op_sel_hi:[1,0]
	v_cvt_pk_bf16_f32 v4, v4, v5

; #define LAS __attribute__((address_space(3)))
; template <bool LOCAL>
; __device__ __forceinline__ void na_unit(const bf16* P, const bf16* VT, bf16* YCAT, const LAS float* rpb_l, LAS bf16* buf, int b, int gr, int hp, int qblk, int tid) {
;     ...
;     const int lane = tid & 63, wv = tid >> 6, fr = lane & 15, fq = lane >> 4, hh = wv >> 2, qb = wv & 3, h = 2 * hp + hh;
;     const int qrow0 = LOCAL ? NCTX + b * SEQ + gr * 64 + 16 * qb : b * CTXL + qblk * 64 + 16 * qb;
;     const int r0 = min(max(gr - 4, 0), 24);
;     const int kc0 = qb == 0 ? 0 : qb == 1 ? 8 : qb == 2 ? 24 : 32;
;     const int qcol = 16 * qb + fr, cs = min(max(qcol - 8, 0), 48);
;     const LAS float* rpb = rpb_l + h * 15 * 31;
;     v4u ld[2][2];
;     const int lrow = (tid >> 3) & 63, lseg = tid & 7;
;     ...
;     bf16x8 qf[2];
; #pragma unroll
;     for (int ks = 0; ks < 2; ++ks) qf[ks] = *(const bf16x8*)(P + (size_t)(qrow0 + fr) * DINP + h * 64 + 32 * ks + 8 * fq);
;     f32x4 sl[16], sc[16];
;     float m = -1.0e30f, lsum = 0.f;
;     f32x4 o[4];
; #pragma unroll
;     for (int dt = 0; dt < 4; ++dt) o[dt] = (f32x4){0.f, 0.f, 0.f, 0.f};
;     NA_ISSUE(0); NA_ISSUE(1); NA_STORE(0);
;     __syncthreads();
; #pragma unroll
;     for (int sidx = 0; sidx < 2 * NCH; ++sidx) {
;         if (sidx + 2 < 2 * NCH) NA_ISSUE(sidx + 2);
;         const LAS bf16* cb = buf + (sidx & 1) * 9216 + hh * 4608;
;         if (sidx < NCH) {
;             const int c = sidx;
;             if (LOCAL && c < 8) {
; #pragma unroll
;                 for (int t2 = 0; t2 < 2; ++t2) {
;                     const LAS bf16* kp = cb + (kc0 + 16 * t2 + fr) * 72 + 8 * fq;
;                     f32x4 acc = {0.f, 0.f, 0.f, 0.f};
;                     acc = __builtin_amdgcn_mfma_f32_16x16x32_bf16(*(const LAS bf16x8*)(kp), qf[0], acc, 0, 0, 0);
;                     acc = __builtin_amdgcn_mfma_f32_16x16x32_bf16(*(const LAS bf16x8*)(kp + 32), qf[1], acc, 0, 0, 0);
;                     const LAS float* rb = rpb + (r0 + c - gr + 7) * 31 + 15 - qcol;
; #pragma unroll
;                     for (int e = 0; e < 4; ++e) { const int kcol = kc0 + 16 * t2 + 4 * fq + e; const bool ok = (kcol >= cs) && (kcol < cs + 16);
;                         const float sv = ok ? acc[e] * 0.125f + rb[ok ? kcol : qcol] : -1.0e30f; acc[e] = sv; m = fmaxf(m, sv); }
;                     sl[2 * (c < 8 ? c : 0) + t2] = acc; }
.LBB0_2659:
	s_or_b64 exec, exec, s[0:1]
	s_bfe_u32 s19, s80, 0x50002
	v_sub_u32_e64 v3, s19, 4 clamp
	s_ashr_i32 s17, s80, 7
	v_readfirstlane_b32 s0, v3
	s_lshl_b32 s26, s17, 11
	s_min_u32 s20, s0, 24
	s_add_i32 s14, s26, 0x1000
	s_lshl_b32 s15, s20, 6
	s_or_b32 s16, s15, s14
	v_mov_b64_e32 v[18:19], s[8:9]
	v_and_b32_e32 v32, 7, v94
	v_or_b32_e32 v3, s16, v89
	s_and_b32 s18, s80, 3
	v_mad_i64_i32 v[4:5], s[0:1], v3, s72, v[18:19]
	v_lshlrev_b32_e32 v26, 4, v32
	v_mov_b32_e32 v27, v71
	v_lshl_add_u64 v[4:5], v[4:5], 0, v[26:27]
	s_lshl_b32 s2, s18, 8
	v_lshl_add_u64 v[4:5], v[4:5], 0, s[2:3]
	global_load_dwordx4 v[10:13], v[4:5], off offset:1024
	global_load_dwordx4 v[14:17], v[4:5], off offset:1152
	s_lshl_b32 s0, s19, 6
	v_lshl_or_b32 v31, v2, 4, v90
	v_lshl_add_u32 v33, s18, 1, v93
	s_or_b32 s0, s14, s0
	v_mad_u32_u24 v2, v89, s73, 0
	v_lshlrev_b32_e32 v72, 6, v33
	s_add_i32 s50, s26, 0x1040
	v_or_b32_e32 v74, s0, v31
	v_add_u32_e32 v75, v2, v26
	v_ashrrev_i32_e32 v73, 31, v72
	v_or_b32_e32 v4, s50, v89
	v_mad_i64_i32 v[2:3], s[0:1], v74, s72, v[18:19]
	v_add_u32_e32 v4, s15, v4
	v_lshl_add_u64 v[2:3], v[72:73], 1, v[2:3]
	v_mad_i64_i32 v[4:5], s[0:1], v4, s72, v[18:19]
	v_lshl_add_u64 v[2:3], v[2:3], 0, v[70:71]
	v_lshl_add_u64 v[20:21], v[4:5], 0, v[26:27]
	global_load_dwordx4 v[6:9], v[2:3], off
	s_nop 0
	global_load_dwordx4 v[2:5], v[2:3], off offset:64
	s_or_b32 s14, s26, s15
	s_addk_i32 s14, 0x1080
	v_or_b32_e32 v24, s14, v89
	v_mad_i64_i32 v[28:29], s[0:1], v24, s72, v[18:19]
	v_lshl_add_u64 v[26:27], v[28:29], 0, v[26:27]
	v_lshl_add_u64 v[22:23], v[20:21], 0, s[2:3]
	v_lshl_add_u64 v[26:27], v[26:27], 0, s[2:3]
	s_mov_b32 s100, 0x60000
	s_mov_b32 s101, 0
	v_lshl_add_u64 v[248:249], v[22:23], 0, s[100:101]
	global_load_dwordx4 v[18:21], v[22:23], off offset:1024
	s_nop 0
	global_load_dwordx4 v[22:25], v[22:23], off offset:1152
	global_load_dword v250, v[248:249], off offset:1024
	global_load_dword v251, v[248:249], off offset:1152
	v_add_u32_e32 v30, v87, v70
	v_add_u32_e32 v34, v91, v90
	v_mad_u32_u24 v36, v34, s73, v30
	s_movk_i32 s0, 0x744
	v_mul_lo_u32 v33, v33, s0
	s_sub_i32 s0, s20, s19
	s_mulk_i32 s0, 0x7c
	v_sub_u32_e64 v35, v31, 8 clamp
	s_add_i32 s0, s0, 0
	v_min_u32_e32 v35, 48, v35
	v_lshlrev_b32_e32 v77, 2, v92
	v_add_u32_e32 v33, s0, v33
	v_lshlrev_b32_e32 v31, 2, v31
	v_sub_u32_e32 v31, v33, v31
	v_add_u32_e32 v33, v91, v77
	v_cmp_ge_u32_e32 vcc, v33, v35
	v_mov_b32_e32 v92, 0xf149f2ca
	v_lshl_add_u32 v31, v33, 2, v31
	v_mov_b32_e32 v93, 0xf149f2ca
	s_waitcnt vmcnt(7)
	ds_write_b128 v75, v[10:13]
	s_waitcnt vmcnt(6)
	ds_write_b128 v75, v[14:17] offset:9216
	s_waitcnt lgkmcnt(0)
	s_barrier
	ds_read_b32 v240, v31 offset:37792
	ds_read_b32 v241, v31 offset:37796
	ds_read_b32 v242, v31 offset:37800
	ds_read_b32 v243, v31 offset:37804
	ds_read_b32 v244, v31 offset:37856
	ds_read_b32 v245, v31 offset:37860
	ds_read_b32 v246, v31 offset:37864
	ds_read_b32 v247, v31 offset:37868
	v_lshl_add_u64 v[248:249], v[26:27], 0, s[100:101]
	global_load_dwordx4 v[10:13], v[26:27], off offset:1024
	global_load_dwordx4 v[14:17], v[26:27], off offset:1152
	global_load_dword v250, v[248:249], off offset:1024
	global_load_dword v251, v[248:249], off offset:1152
	ds_read_b128 v[26:29], v36
	ds_read_b128 v[38:41], v36 offset:64
	s_waitcnt vmcnt(9) lgkmcnt(1)
	v_mfma_f32_16x16x32_bf16 v[26:29], v[26:29], v[6:9], 0
	v_add_u32_e32 v36, 16, v35
	v_cmp_lt_u32_e64 s[0:1], v33, v36
	s_and_b64 s[28:29], vcc, s[0:1]
	s_waitcnt vmcnt(8) lgkmcnt(0)
	v_mfma_f32_16x16x32_bf16 v[26:29], v[38:41], v[2:5], v[26:29]
	s_nop 2
	s_waitcnt lgkmcnt(0)
	s_nop 3
	v_fmac_f32_e32 v240, 0x3e000000, v26
	v_cndmask_b32_e64 v93, v93, v240, s[28:29]
	s_nop 4
	v_or_b32_e32 v26, 1, v33
	v_cmp_ge_u32_e32 vcc, v26, v35
	v_cmp_lt_u32_e64 s[0:1], v26, v36
	s_and_b64 s[30:31], vcc, s[0:1]
	s_nop 2
	s_waitcnt lgkmcnt(0)
	v_fmac_f32_e32 v241, 0x3e000000, v27
	v_cndmask_b32_e64 v92, v92, v241, s[30:31]
	v_or_b32_e32 v26, 2, v33
	v_cmp_ge_u32_e32 vcc, v26, v35
	v_cmp_lt_u32_e64 s[0:1], v26, v36
	s_and_b64 s[34:35], vcc, s[0:1]
	v_mov_b32_e32 v94, 0xf149f2ca
	v_mov_b32_e32 v95, 0xf149f2ca
	s_nop 2
	s_waitcnt lgkmcnt(0)
	v_fmac_f32_e32 v242, 0x3e000000, v28
	v_cndmask_b32_e64 v95, v95, v242, s[34:35]
	v_or_b32_e32 v26, 3, v33
	v_cmp_ge_u32_e32 vcc, v26, v35
	v_cmp_lt_u32_e64 s[0:1], v26, v36
	s_and_b64 s[36:37], vcc, s[0:1]
	s_nop 2
	s_waitcnt lgkmcnt(0)
	v_fmac_f32_e32 v243, 0x3e000000, v29
	v_cndmask_b32_e64 v94, v94, v243, s[36:37]
	v_add_u32_e32 v37, 16, v91
	v_add_u32_e32 v33, v37, v90
	v_mad_u32_u24 v38, v33, s73, v30
	ds_read_b128 v[26:29], v38
	ds_read_b128 v[38:41], v38 offset:64
	v_add_u32_e32 v37, v37, v77
	v_cmp_ge_u32_e32 vcc, v37, v35
	v_cmp_lt_u32_e64 s[0:1], v37, v36
	s_waitcnt lgkmcnt(1)
	v_mfma_f32_16x16x32_bf16 v[26:29], v[26:29], v[6:9], 0
	s_and_b64 s[38:39], vcc, s[0:1]
	v_mov_b32_e32 v96, 0xf149f2ca
	v_mov_b32_e32 v97, 0xf149f2ca
	s_waitcnt lgkmcnt(0)
	v_mfma_f32_16x16x32_bf16 v[26:29], v[38:41], v[2:5], v[26:29]
	s_nop 2
	s_waitcnt lgkmcnt(0)
	s_nop 3
	v_fmac_f32_e32 v244, 0x3e000000, v26
	v_cndmask_b32_e64 v97, v97, v244, s[38:39]
	s_nop 4
	v_or_b32_e32 v26, 1, v37
	v_cmp_ge_u32_e32 vcc, v26, v35
	v_cmp_lt_u32_e64 s[0:1], v26, v36
	s_and_b64 s[44:45], vcc, s[0:1]
	s_nop 2
	s_waitcnt lgkmcnt(0)
	v_fmac_f32_e32 v245, 0x3e000000, v27
	v_cndmask_b32_e64 v96, v96, v245, s[44:45]
	v_or_b32_e32 v26, 2, v37
	v_cmp_ge_u32_e32 vcc, v26, v35
	v_cmp_lt_u32_e64 s[0:1], v26, v36
	s_and_b64 s[46:47], vcc, s[0:1]
	v_mov_b32_e32 v98, 0xf149f2ca
	v_mov_b32_e32 v100, 0xf149f2ca
	s_nop 2
	s_waitcnt lgkmcnt(0)
	v_fmac_f32_e32 v246, 0x3e000000, v28
	v_cndmask_b32_e64 v100, v100, v246, s[46:47]
	v_or_b32_e32 v26, 3, v37
	v_cmp_ge_u32_e32 vcc, v26, v35
	v_cmp_lt_u32_e64 s[0:1], v26, v36
	s_and_b64 s[66:67], vcc, s[0:1]
	s_nop 2
	s_waitcnt lgkmcnt(0)
	v_fmac_f32_e32 v247, 0x3e000000, v29
	v_cndmask_b32_e64 v98, v98, v247, s[66:67]
	v_mul_u32_u24_e32 v27, 0x90, v34
	v_lshlrev_b32_e32 v26, 3, v32
	v_add_u32_e32 v32, v30, v27
	s_waitcnt vmcnt(7)
	ds_write_b128 v75, v[18:21] offset:18432
	s_waitcnt vmcnt(6)
	ds_write_b128 v75, v[22:25] offset:27648
	s_waitcnt lgkmcnt(0)
	s_barrier
; #define LAS __attribute__((address_space(3)))
; template <bool LOCAL>
; __device__ __forceinline__ void na_unit(const bf16* P, const bf16* VT, bf16* YCAT, const LAS float* rpb_l, LAS bf16* buf, int b, int gr, int hp, int qblk, int tid) {
;     ...
;     for (int sidx = 0; sidx < 2 * NCH; ++sidx) {
;         if (sidx + 2 < 2 * NCH) NA_ISSUE(sidx + 2);
;         const LAS bf16* cb = buf + (sidx & 1) * 9216 + hh * 4608;
;         if (sidx < NCH) {
;             const int c = sidx;
;             if (LOCAL && c < 8) {
; #pragma unroll
;                 for (int t2 = 0; t2 < 2; ++t2) {
;                     const LAS bf16* kp = cb + (kc0 + 16 * t2 + fr) * 72 + 8 * fq;
;                     f32x4 acc = {0.f, 0.f, 0.f, 0.f};
;                     acc = __builtin_amdgcn_mfma_f32_16x16x32_bf16(*(const LAS bf16x8*)(kp), qf[0], acc, 0, 0, 0);
;                     acc = __builtin_amdgcn_mfma_f32_16x16x32_bf16(*(const LAS bf16x8*)(kp + 32), qf[1], acc, 0, 0, 0);
;                     const LAS float* rb = rpb + (r0 + c - gr + 7) * 31 + 15 - qcol;
; #pragma unroll
;                     for (int e = 0; e < 4; ++e) { const int kcol = kc0 + 16 * t2 + 4 * fq + e; const bool ok = (kcol >= cs) && (kcol < cs + 16);
;                         const float sv = ok ? acc[e] * 0.125f + rb[ok ? kcol : qcol] : -1.0e30f; acc[e] = sv; m = fmaxf(m, sv); }
;                     sl[2 * (c < 8 ? c : 0) + t2] = acc; }
	ds_read_b32 v240, v31 offset:37916
	ds_read_b32 v241, v31 offset:37920
	ds_read_b32 v242, v31 offset:37924
	ds_read_b32 v243, v31 offset:37928
	ds_read_b32 v244, v31 offset:37980
	ds_read_b32 v245, v31 offset:37984
	ds_read_b32 v246, v31 offset:37988
	ds_read_b32 v247, v31 offset:37992
	ds_read_b128 v[18:21], v32 offset:18432
	s_add_i32 s26, s26, s15
	s_add_i32 s0, s26, 0x10c0
	v_or_b32_e32 v24, s0, v89
	v_mov_b64_e32 v[22:23], s[8:9]
	s_lshl_b32 s1, s18, 7
	v_mad_i64_i32 v[22:23], s[18:19], v24, s72, v[22:23]
	v_lshlrev_b32_e32 v70, 1, v26
	v_lshl_add_u64 v[22:23], v[22:23], 0, v[70:71]
	s_lshl_b32 s2, s1, 1
	v_lshl_add_u64 v[22:23], v[22:23], 0, s[2:3]
	ds_read_b128 v[26:29], v32 offset:18496
	s_waitcnt lgkmcnt(1)
	v_mfma_f32_16x16x32_bf16 v[34:37], v[18:21], v[6:9], 0
	v_lshl_add_u64 v[248:249], v[22:23], 0, s[100:101]
	global_load_dwordx4 v[18:21], v[22:23], off offset:1024
	s_nop 0
	global_load_dwordx4 v[22:25], v[22:23], off offset:1152
	global_load_dword v250, v[248:249], off offset:1024
	global_load_dword v251, v[248:249], off offset:1152
	v_mov_b32_e32 v99, 0xf149f2ca
	v_mov_b32_e32 v101, 0xf149f2ca
	s_waitcnt lgkmcnt(0)
	v_mfma_f32_16x16x32_bf16 v[26:29], v[26:29], v[2:5], v[34:37]
	s_nop 2
	s_waitcnt lgkmcnt(0)
	s_nop 3
	v_fmac_f32_e32 v240, 0x3e000000, v26
	v_cndmask_b32_e64 v101, v101, v240, s[28:29]
	s_nop 2
	s_waitcnt lgkmcnt(0)
	s_nop 0
	v_fmac_f32_e32 v241, 0x3e000000, v27
	v_cndmask_b32_e64 v99, v99, v241, s[30:31]
	v_mov_b32_e32 v102, 0xf149f2ca
	v_mov_b32_e32 v103, 0xf149f2ca
	s_nop 2
	s_waitcnt lgkmcnt(0)
	v_fmac_f32_e32 v242, 0x3e000000, v28
	v_cndmask_b32_e64 v103, v103, v242, s[34:35]
	s_nop 2
	s_waitcnt lgkmcnt(0)
	v_fmac_f32_e32 v243, 0x3e000000, v29
	v_cndmask_b32_e64 v102, v102, v243, s[36:37]
	v_mul_u32_u24_e32 v26, 0x90, v33
	v_add_u32_e32 v33, v30, v26
	ds_read_b128 v[26:29], v33 offset:18432
	ds_read_b128 v[34:37], v33 offset:18496
	v_mov_b32_e32 v104, 0xf149f2ca
	v_mov_b32_e32 v106, 0xf149f2ca
	s_waitcnt lgkmcnt(1)
	v_mfma_f32_16x16x32_bf16 v[26:29], v[26:29], v[6:9], 0
	s_waitcnt lgkmcnt(0)
	v_mfma_f32_16x16x32_bf16 v[26:29], v[34:37], v[2:5], v[26:29]
	s_nop 2
	s_waitcnt lgkmcnt(0)
	s_nop 3
	v_fmac_f32_e32 v244, 0x3e000000, v26
	v_cndmask_b32_e64 v106, v106, v244, s[38:39]
	s_nop 2
	s_waitcnt lgkmcnt(0)
	s_nop 0
	v_fmac_f32_e32 v245, 0x3e000000, v27
	v_cndmask_b32_e64 v104, v104, v245, s[44:45]
	v_mov_b32_e32 v108, 0xf149f2ca
	v_mov_b32_e32 v110, 0xf149f2ca
	s_nop 2
	s_waitcnt lgkmcnt(0)
	v_fmac_f32_e32 v246, 0x3e000000, v28
	v_cndmask_b32_e64 v110, v110, v246, s[46:47]
	s_nop 2
	s_waitcnt lgkmcnt(0)
	v_fmac_f32_e32 v247, 0x3e000000, v29
	v_cndmask_b32_e64 v108, v108, v247, s[66:67]
	s_waitcnt vmcnt(7)
	ds_write_b128 v75, v[10:13]
	s_waitcnt vmcnt(6)
	ds_write_b128 v75, v[14:17] offset:9216
	s_waitcnt lgkmcnt(0)
	s_barrier
	ds_read_b32 v240, v31 offset:38040
	ds_read_b32 v241, v31 offset:38044
	ds_read_b32 v242, v31 offset:38048
	ds_read_b32 v243, v31 offset:38052
	ds_read_b32 v244, v31 offset:38104
	ds_read_b32 v245, v31 offset:38108
	ds_read_b32 v246, v31 offset:38112
	ds_read_b32 v247, v31 offset:38116
	ds_read_b128 v[10:13], v32
	ds_read_b128 v[26:29], v32 offset:64
	s_add_i32 s18, s26, 0x1100
	v_or_b32_e32 v16, s18, v89
	v_mov_b64_e32 v[14:15], s[8:9]
	v_mad_i64_i32 v[14:15], s[20:21], v16, s72, v[14:15]
	v_lshl_add_u64 v[14:15], v[14:15], 0, v[70:71]
	v_lshl_add_u64 v[14:15], v[14:15], 0, s[2:3]
	s_waitcnt lgkmcnt(1)
	v_mfma_f32_16x16x32_bf16 v[34:37], v[10:13], v[6:9], 0
	v_lshl_add_u64 v[248:249], v[14:15], 0, s[100:101]
	global_load_dwordx4 v[10:13], v[14:15], off offset:1024
	s_nop 0
	global_load_dwordx4 v[14:17], v[14:15], off offset:1152
	global_load_dword v250, v[248:249], off offset:1024
	global_load_dword v251, v[248:249], off offset:1152
	v_mov_b32_e32 v105, 0xf149f2ca
	v_mov_b32_e32 v107, 0xf149f2ca
	s_waitcnt lgkmcnt(0)
	v_mfma_f32_16x16x32_bf16 v[26:29], v[26:29], v[2:5], v[34:37]
	s_nop 2
	s_waitcnt lgkmcnt(0)
	s_nop 3
	v_fmac_f32_e32 v240, 0x3e000000, v26
	v_cndmask_b32_e64 v107, v107, v240, s[28:29]
	s_nop 2
	s_waitcnt lgkmcnt(0)
	s_nop 0
	v_fmac_f32_e32 v241, 0x3e000000, v27
	v_cndmask_b32_e64 v105, v105, v241, s[30:31]
	v_mov_b32_e32 v109, 0xf149f2ca
	v_mov_b32_e32 v111, 0xf149f2ca
	s_nop 2
	s_waitcnt lgkmcnt(0)
	v_fmac_f32_e32 v242, 0x3e000000, v28
	v_cndmask_b32_e64 v111, v111, v242, s[34:35]
	s_nop 2
	s_waitcnt lgkmcnt(0)
	v_fmac_f32_e32 v243, 0x3e000000, v29
	v_cndmask_b32_e64 v109, v109, v243, s[36:37]
	ds_read_b128 v[26:29], v33
	ds_read_b128 v[34:37], v33 offset:64
	v_mov_b32_e32 v112, 0xf149f2ca
	v_mov_b32_e32 v114, 0xf149f2ca
	s_waitcnt lgkmcnt(1)
	v_mfma_f32_16x16x32_bf16 v[26:29], v[26:29], v[6:9], 0
	s_waitcnt lgkmcnt(0)
	v_mfma_f32_16x16x32_bf16 v[26:29], v[34:37], v[2:5], v[26:29]
	s_nop 2
	s_waitcnt lgkmcnt(0)
	s_nop 3
	v_fmac_f32_e32 v244, 0x3e000000, v26
	v_cndmask_b32_e64 v114, v114, v244, s[38:39]
	s_nop 2
	s_waitcnt lgkmcnt(0)
	s_nop 0
	v_fmac_f32_e32 v245, 0x3e000000, v27
	v_cndmask_b32_e64 v112, v112, v245, s[44:45]
	v_mov_b32_e32 v113, 0xf149f2ca
	v_mov_b32_e32 v117, 0xf149f2ca
	s_nop 2
	s_waitcnt lgkmcnt(0)
	v_fmac_f32_e32 v246, 0x3e000000, v28
	v_cndmask_b32_e64 v117, v117, v246, s[46:47]
	s_nop 2
	s_waitcnt lgkmcnt(0)
	v_fmac_f32_e32 v247, 0x3e000000, v29
	v_cndmask_b32_e64 v113, v113, v247, s[66:67]
	s_waitcnt vmcnt(7)
	ds_write_b128 v75, v[18:21] offset:18432
	s_waitcnt vmcnt(6)
	ds_write_b128 v75, v[22:25] offset:27648
	s_waitcnt lgkmcnt(0)
	s_barrier
; #define LAS __attribute__((address_space(3)))
; template <bool LOCAL>
; __device__ __forceinline__ void na_unit(const bf16* P, const bf16* VT, bf16* YCAT, const LAS float* rpb_l, LAS bf16* buf, int b, int gr, int hp, int qblk, int tid) {
;     ...
;     for (int sidx = 0; sidx < 2 * NCH; ++sidx) {
;         if (sidx + 2 < 2 * NCH) NA_ISSUE(sidx + 2);
;         const LAS bf16* cb = buf + (sidx & 1) * 9216 + hh * 4608;
;         if (sidx < NCH) {
;             const int c = sidx;
;             if (LOCAL && c < 8) {
; #pragma unroll
;                 for (int t2 = 0; t2 < 2; ++t2) {
;                     const LAS bf16* kp = cb + (kc0 + 16 * t2 + fr) * 72 + 8 * fq;
;                     f32x4 acc = {0.f, 0.f, 0.f, 0.f};
;                     acc = __builtin_amdgcn_mfma_f32_16x16x32_bf16(*(const LAS bf16x8*)(kp), qf[0], acc, 0, 0, 0);
;                     acc = __builtin_amdgcn_mfma_f32_16x16x32_bf16(*(const LAS bf16x8*)(kp + 32), qf[1], acc, 0, 0, 0);
;                     const LAS float* rb = rpb + (r0 + c - gr + 7) * 31 + 15 - qcol;
; #pragma unroll
;                     for (int e = 0; e < 4; ++e) { const int kcol = kc0 + 16 * t2 + 4 * fq + e; const bool ok = (kcol >= cs) && (kcol < cs + 16);
;                         const float sv = ok ? acc[e] * 0.125f + rb[ok ? kcol : qcol] : -1.0e30f; acc[e] = sv; m = fmaxf(m, sv); }
;                     sl[2 * (c < 8 ? c : 0) + t2] = acc; }
	ds_read_b32 v240, v31 offset:38164
	ds_read_b32 v241, v31 offset:38168
	ds_read_b32 v242, v31 offset:38172
	ds_read_b32 v243, v31 offset:38176
	ds_read_b32 v244, v31 offset:38228
	ds_read_b32 v245, v31 offset:38232
	ds_read_b32 v246, v31 offset:38236
	ds_read_b32 v247, v31 offset:38240
	ds_read_b128 v[18:21], v32 offset:18432
	ds_read_b128 v[26:29], v32 offset:18496
	s_add_i32 s20, s26, 0x1140
	v_or_b32_e32 v24, s20, v89
	v_mov_b64_e32 v[22:23], s[8:9]
	v_mad_i64_i32 v[22:23], s[22:23], v24, s72, v[22:23]
	v_lshl_add_u64 v[22:23], v[22:23], 0, v[70:71]
	v_lshl_add_u64 v[22:23], v[22:23], 0, s[2:3]
	s_waitcnt lgkmcnt(1)
	v_mfma_f32_16x16x32_bf16 v[34:37], v[18:21], v[6:9], 0
	v_lshl_add_u64 v[248:249], v[22:23], 0, s[100:101]
	global_load_dwordx4 v[18:21], v[22:23], off offset:1024
	s_nop 0
	global_load_dwordx4 v[22:25], v[22:23], off offset:1152
	global_load_dword v250, v[248:249], off offset:1024
	global_load_dword v251, v[248:249], off offset:1152
	v_mov_b32_e32 v115, 0xf149f2ca
	v_mov_b32_e32 v116, 0xf149f2ca
	s_waitcnt lgkmcnt(0)
	v_mfma_f32_16x16x32_bf16 v[26:29], v[26:29], v[2:5], v[34:37]
	s_nop 2
	s_waitcnt lgkmcnt(0)
	s_nop 3
	v_fmac_f32_e32 v240, 0x3e000000, v26
	v_cndmask_b32_e64 v116, v116, v240, s[28:29]
	s_nop 2
	s_waitcnt lgkmcnt(0)
	s_nop 0
	v_fmac_f32_e32 v241, 0x3e000000, v27
	v_cndmask_b32_e64 v115, v115, v241, s[30:31]
	v_mov_b32_e32 v118, 0xf149f2ca
	v_mov_b32_e32 v119, 0xf149f2ca
	s_nop 2
	s_waitcnt lgkmcnt(0)
	v_fmac_f32_e32 v242, 0x3e000000, v28
	v_cndmask_b32_e64 v119, v119, v242, s[34:35]
	s_nop 2
	s_waitcnt lgkmcnt(0)
	v_fmac_f32_e32 v243, 0x3e000000, v29
	v_cndmask_b32_e64 v118, v118, v243, s[36:37]
	ds_read_b128 v[26:29], v33 offset:18432
	ds_read_b128 v[34:37], v33 offset:18496
	v_mov_b32_e32 v120, 0xf149f2ca
	v_mov_b32_e32 v122, 0xf149f2ca
	s_waitcnt lgkmcnt(1)
	v_mfma_f32_16x16x32_bf16 v[26:29], v[26:29], v[6:9], 0
	s_waitcnt lgkmcnt(0)
	v_mfma_f32_16x16x32_bf16 v[26:29], v[34:37], v[2:5], v[26:29]
	s_nop 2
	s_waitcnt lgkmcnt(0)
	s_nop 3
	v_fmac_f32_e32 v244, 0x3e000000, v26
	v_cndmask_b32_e64 v122, v122, v244, s[38:39]
	s_nop 2
	s_waitcnt lgkmcnt(0)
	s_nop 0
	v_fmac_f32_e32 v245, 0x3e000000, v27
	v_cndmask_b32_e64 v120, v120, v245, s[44:45]
	v_mov_b32_e32 v121, 0xf149f2ca
	v_mov_b32_e32 v125, 0xf149f2ca
	s_nop 2
	s_waitcnt lgkmcnt(0)
	v_fmac_f32_e32 v246, 0x3e000000, v28
	v_cndmask_b32_e64 v125, v125, v246, s[46:47]
	s_nop 2
	s_waitcnt lgkmcnt(0)
	v_fmac_f32_e32 v247, 0x3e000000, v29
	v_cndmask_b32_e64 v121, v121, v247, s[66:67]
	s_waitcnt vmcnt(7)
	ds_write_b128 v75, v[10:13]
	s_waitcnt vmcnt(6)
	ds_write_b128 v75, v[14:17] offset:9216
	s_waitcnt lgkmcnt(0)
	s_barrier
	ds_read_b32 v240, v31 offset:38288
	ds_read_b32 v241, v31 offset:38292
	ds_read_b32 v242, v31 offset:38296
	ds_read_b32 v243, v31 offset:38300
	ds_read_b32 v244, v31 offset:38352
	ds_read_b32 v245, v31 offset:38356
	ds_read_b32 v246, v31 offset:38360
	ds_read_b32 v247, v31 offset:38364
	ds_read_b128 v[10:13], v32
	ds_read_b128 v[26:29], v32 offset:64
	s_add_i32 s22, s26, 0x1180
	v_or_b32_e32 v16, s22, v89
	v_mov_b64_e32 v[14:15], s[8:9]
	v_mad_i64_i32 v[14:15], s[24:25], v16, s72, v[14:15]
	v_lshl_add_u64 v[14:15], v[14:15], 0, v[70:71]
	v_lshl_add_u64 v[14:15], v[14:15], 0, s[2:3]
	s_waitcnt lgkmcnt(1)
	v_mfma_f32_16x16x32_bf16 v[34:37], v[10:13], v[6:9], 0
	v_lshl_add_u64 v[248:249], v[14:15], 0, s[100:101]
	global_load_dwordx4 v[10:13], v[14:15], off offset:1024
	s_nop 0
	global_load_dwordx4 v[14:17], v[14:15], off offset:1152
	global_load_dword v250, v[248:249], off offset:1024
	global_load_dword v251, v[248:249], off offset:1152
	v_mov_b32_e32 v123, 0xf149f2ca
	v_mov_b32_e32 v124, 0xf149f2ca
	s_waitcnt lgkmcnt(0)
	v_mfma_f32_16x16x32_bf16 v[26:29], v[26:29], v[2:5], v[34:37]
	s_nop 2
	s_waitcnt lgkmcnt(0)
	s_nop 3
	v_fmac_f32_e32 v240, 0x3e000000, v26
	v_cndmask_b32_e64 v124, v124, v240, s[28:29]
	s_nop 2
	s_waitcnt lgkmcnt(0)
	s_nop 0
	v_fmac_f32_e32 v241, 0x3e000000, v27
	v_cndmask_b32_e64 v123, v123, v241, s[30:31]
	v_mov_b32_e32 v126, 0xf149f2ca
	v_mov_b32_e32 v127, 0xf149f2ca
	s_nop 2
	s_waitcnt lgkmcnt(0)
	v_fmac_f32_e32 v242, 0x3e000000, v28
	v_cndmask_b32_e64 v127, v127, v242, s[34:35]
	s_nop 2
	s_waitcnt lgkmcnt(0)
	v_fmac_f32_e32 v243, 0x3e000000, v29
	v_cndmask_b32_e64 v126, v126, v243, s[36:37]
	ds_read_b128 v[26:29], v33
	ds_read_b128 v[34:37], v33 offset:64
	v_mov_b32_e32 v128, 0xf149f2ca
	v_mov_b32_e32 v130, 0xf149f2ca
	s_waitcnt lgkmcnt(1)
	v_mfma_f32_16x16x32_bf16 v[26:29], v[26:29], v[6:9], 0
	s_waitcnt lgkmcnt(0)
	v_mfma_f32_16x16x32_bf16 v[26:29], v[34:37], v[2:5], v[26:29]
	s_nop 2
	s_waitcnt lgkmcnt(0)
	s_nop 3
	v_fmac_f32_e32 v244, 0x3e000000, v26
	v_cndmask_b32_e64 v130, v130, v244, s[38:39]
	s_nop 2
	s_waitcnt lgkmcnt(0)
	s_nop 0
	v_fmac_f32_e32 v245, 0x3e000000, v27
	v_cndmask_b32_e64 v128, v128, v245, s[44:45]
	v_mov_b32_e32 v129, 0xf149f2ca
	v_mov_b32_e32 v134, 0xf149f2ca
	s_nop 2
	s_waitcnt lgkmcnt(0)
	v_fmac_f32_e32 v246, 0x3e000000, v28
	v_cndmask_b32_e64 v134, v134, v246, s[46:47]
	s_nop 2
	s_waitcnt lgkmcnt(0)
	v_fmac_f32_e32 v247, 0x3e000000, v29
	v_cndmask_b32_e64 v129, v129, v247, s[66:67]
	s_waitcnt vmcnt(7)
	ds_write_b128 v75, v[18:21] offset:18432
	s_waitcnt vmcnt(6)
	ds_write_b128 v75, v[22:25] offset:27648
	s_waitcnt lgkmcnt(0)
	s_barrier
; #define LAS __attribute__((address_space(3)))
; template <bool LOCAL>
; __device__ __forceinline__ void na_unit(const bf16* P, const bf16* VT, bf16* YCAT, const LAS float* rpb_l, LAS bf16* buf, int b, int gr, int hp, int qblk, int tid) {
;     ...
;     for (int sidx = 0; sidx < 2 * NCH; ++sidx) {
;         if (sidx + 2 < 2 * NCH) NA_ISSUE(sidx + 2);
;         const LAS bf16* cb = buf + (sidx & 1) * 9216 + hh * 4608;
;         if (sidx < NCH) {
;             const int c = sidx;
;             if (LOCAL && c < 8) {
; #pragma unroll
;                 for (int t2 = 0; t2 < 2; ++t2) {
;                     const LAS bf16* kp = cb + (kc0 + 16 * t2 + fr) * 72 + 8 * fq;
;                     f32x4 acc = {0.f, 0.f, 0.f, 0.f};
;                     acc = __builtin_amdgcn_mfma_f32_16x16x32_bf16(*(const LAS bf16x8*)(kp), qf[0], acc, 0, 0, 0);
;                     acc = __builtin_amdgcn_mfma_f32_16x16x32_bf16(*(const LAS bf16x8*)(kp + 32), qf[1], acc, 0, 0, 0);
;                     const LAS float* rb = rpb + (r0 + c - gr + 7) * 31 + 15 - qcol;
; #pragma unroll
;                     for (int e = 0; e < 4; ++e) { const int kcol = kc0 + 16 * t2 + 4 * fq + e; const bool ok = (kcol >= cs) && (kcol < cs + 16);
;                         const float sv = ok ? acc[e] * 0.125f + rb[ok ? kcol : qcol] : -1.0e30f; acc[e] = sv; m = fmaxf(m, sv); }
;                     sl[2 * (c < 8 ? c : 0) + t2] = acc; }
;             } else {
;                 const int cc = c - NLOC;
	ds_read_b32 v240, v31 offset:38412
	ds_read_b32 v241, v31 offset:38416
	ds_read_b32 v242, v31 offset:38420
	ds_read_b32 v243, v31 offset:38424
	ds_read_b32 v244, v31 offset:38476
	ds_read_b32 v245, v31 offset:38480
	ds_read_b32 v246, v31 offset:38484
	ds_read_b32 v247, v31 offset:38488
	ds_read_b128 v[18:21], v32 offset:18432
	ds_read_b128 v[26:29], v32 offset:18496
	s_add_i32 s24, s26, 0x11c0
	v_or_b32_e32 v24, s24, v89
	v_mov_b64_e32 v[22:23], s[8:9]
	v_mad_i64_i32 v[22:23], s[26:27], v24, s72, v[22:23]
	v_lshl_add_u64 v[22:23], v[22:23], 0, v[70:71]
	v_lshl_add_u64 v[22:23], v[22:23], 0, s[2:3]
	s_waitcnt lgkmcnt(1)
	v_mfma_f32_16x16x32_bf16 v[34:37], v[18:21], v[6:9], 0
	global_load_dwordx4 v[18:21], v[22:23], off offset:1024
	s_nop 0
	global_load_dwordx4 v[22:25], v[22:23], off offset:1152
	v_mov_b32_e32 v131, 0xf149f2ca
	v_mov_b32_e32 v132, 0xf149f2ca
	s_waitcnt lgkmcnt(0)
	v_mfma_f32_16x16x32_bf16 v[26:29], v[26:29], v[2:5], v[34:37]
	s_nop 2
	s_waitcnt lgkmcnt(0)
	s_nop 3
	v_fmac_f32_e32 v240, 0x3e000000, v26
	v_cndmask_b32_e64 v132, v132, v240, s[28:29]
	s_nop 2
	s_waitcnt lgkmcnt(0)
	s_nop 0
	v_fmac_f32_e32 v241, 0x3e000000, v27
	v_cndmask_b32_e64 v131, v131, v241, s[30:31]
	v_mov_b32_e32 v135, 0xf149f2ca
	v_mov_b32_e32 v136, 0xf149f2ca
	s_nop 2
	s_waitcnt lgkmcnt(0)
	v_fmac_f32_e32 v242, 0x3e000000, v28
	v_cndmask_b32_e64 v136, v136, v242, s[34:35]
	s_nop 2
	s_waitcnt lgkmcnt(0)
	v_fmac_f32_e32 v243, 0x3e000000, v29
	v_cndmask_b32_e64 v135, v135, v243, s[36:37]
	ds_read_b128 v[26:29], v33 offset:18432
	ds_read_b128 v[34:37], v33 offset:18496
	v_mov_b32_e32 v138, 0xf149f2ca
	v_mov_b32_e32 v140, 0xf149f2ca
	s_waitcnt lgkmcnt(1)
	v_mfma_f32_16x16x32_bf16 v[26:29], v[26:29], v[6:9], 0
	s_waitcnt lgkmcnt(0)
	v_mfma_f32_16x16x32_bf16 v[26:29], v[34:37], v[2:5], v[26:29]
	s_nop 2
	s_waitcnt lgkmcnt(0)
	s_nop 3
	v_fmac_f32_e32 v244, 0x3e000000, v26
	v_cndmask_b32_e64 v140, v140, v244, s[38:39]
	s_nop 2
	s_waitcnt lgkmcnt(0)
	s_nop 0
	v_fmac_f32_e32 v245, 0x3e000000, v27
	v_cndmask_b32_e64 v138, v138, v245, s[44:45]
	v_mov_b32_e32 v139, 0xf149f2ca
	v_mov_b32_e32 v143, 0xf149f2ca
	s_nop 2
	s_waitcnt lgkmcnt(0)
	v_fmac_f32_e32 v246, 0x3e000000, v28
	v_cndmask_b32_e64 v143, v143, v246, s[46:47]
	s_nop 2
	s_waitcnt lgkmcnt(0)
	v_fmac_f32_e32 v247, 0x3e000000, v29
	v_cndmask_b32_e64 v139, v139, v247, s[66:67]
	s_waitcnt vmcnt(5)
	ds_write_b128 v75, v[10:13]
	s_waitcnt vmcnt(4)
	ds_write_b128 v75, v[14:17] offset:9216
	s_waitcnt lgkmcnt(0)
	s_barrier
	ds_read_b32 v240, v31 offset:38536
	ds_read_b32 v241, v31 offset:38540
	ds_read_b32 v242, v31 offset:38544
	ds_read_b32 v243, v31 offset:38548
	ds_read_b32 v244, v31 offset:38600
	ds_read_b32 v245, v31 offset:38604
	ds_read_b32 v246, v31 offset:38608
	ds_read_b32 v247, v31 offset:38612
	ds_read_b128 v[10:13], v32
	ds_read_b128 v[26:29], v32 offset:64
	s_lshl_b32 s26, s17, 8
	v_or_b32_e32 v34, s26, v89
	v_mov_b64_e32 v[14:15], s[8:9]
	v_mad_i64_i32 v[14:15], s[52:53], v34, s72, v[14:15]
	v_lshl_add_u64 v[14:15], v[14:15], 0, v[70:71]
	v_lshl_add_u64 v[14:15], v[14:15], 0, s[2:3]
	s_waitcnt lgkmcnt(1)
	v_mfma_f32_16x16x32_bf16 v[36:39], v[10:13], v[6:9], 0
	v_lshl_add_u64 v[248:249], v[14:15], 0, s[100:101]
	global_load_dwordx4 v[10:13], v[14:15], off offset:1024
	s_nop 0
	global_load_dwordx4 v[14:17], v[14:15], off offset:1152
	global_load_dword v250, v[248:249], off offset:1024
	global_load_dword v251, v[248:249], off offset:1152
	v_mov_b32_e32 v141, 0xf149f2ca
	v_mov_b32_e32 v142, 0xf149f2ca
	s_waitcnt lgkmcnt(0)
	v_mfma_f32_16x16x32_bf16 v[26:29], v[26:29], v[2:5], v[36:39]
	s_nop 2
	s_waitcnt lgkmcnt(0)
	s_nop 3
	v_fmac_f32_e32 v240, 0x3e000000, v26
	v_cndmask_b32_e64 v142, v142, v240, s[28:29]
	s_nop 2
	s_waitcnt lgkmcnt(0)
	s_nop 0
	v_fmac_f32_e32 v241, 0x3e000000, v27
	v_cndmask_b32_e64 v141, v141, v241, s[30:31]
	v_mov_b32_e32 v144, 0xf149f2ca
	v_mov_b32_e32 v145, 0xf149f2ca
	s_nop 2
	s_waitcnt lgkmcnt(0)
	v_fmac_f32_e32 v242, 0x3e000000, v28
	v_cndmask_b32_e64 v145, v145, v242, s[34:35]
	s_nop 2
	s_waitcnt lgkmcnt(0)
	v_fmac_f32_e32 v243, 0x3e000000, v29
	v_cndmask_b32_e64 v144, v144, v243, s[36:37]
	ds_read_b128 v[26:29], v33
	ds_read_b128 v[36:39], v33 offset:64
	v_mov_b32_e32 v146, 0xf149f2ca
	v_mov_b32_e32 v148, 0xf149f2ca
	s_waitcnt lgkmcnt(1)
	v_mfma_f32_16x16x32_bf16 v[26:29], v[26:29], v[6:9], 0
	s_waitcnt lgkmcnt(0)
	v_mfma_f32_16x16x32_bf16 v[26:29], v[36:39], v[2:5], v[26:29]
	s_nop 2
	s_waitcnt lgkmcnt(0)
	s_nop 3
	v_fmac_f32_e32 v244, 0x3e000000, v26
	v_cndmask_b32_e64 v148, v148, v244, s[38:39]
	s_nop 2
	s_waitcnt lgkmcnt(0)
	s_nop 0
	v_fmac_f32_e32 v245, 0x3e000000, v27
	v_cndmask_b32_e64 v146, v146, v245, s[44:45]
	v_mov_b32_e32 v147, 0xf149f2ca
	v_mov_b32_e32 v151, 0xf149f2ca
	s_nop 2
	s_waitcnt lgkmcnt(0)
	v_fmac_f32_e32 v246, 0x3e000000, v28
	v_cndmask_b32_e64 v151, v151, v246, s[46:47]
	s_nop 2
	s_waitcnt lgkmcnt(0)
	v_fmac_f32_e32 v247, 0x3e000000, v29
	v_cndmask_b32_e64 v147, v147, v247, s[66:67]
	s_waitcnt vmcnt(5)
	ds_write_b128 v75, v[18:21] offset:18432
	s_waitcnt vmcnt(4)
	ds_write_b128 v75, v[22:25] offset:27648
	s_waitcnt lgkmcnt(0)
	s_barrier
; #define LAS __attribute__((address_space(3)))
; template <bool LOCAL>
; __device__ __forceinline__ void na_unit(const bf16* P, const bf16* VT, bf16* YCAT, const LAS float* rpb_l, LAS bf16* buf, int b, int gr, int hp, int qblk, int tid) {
;     ...
;     for (int sidx = 0; sidx < 2 * NCH; ++sidx) {
;         if (sidx + 2 < 2 * NCH) NA_ISSUE(sidx + 2);
;         const LAS bf16* cb = buf + (sidx & 1) * 9216 + hh * 4608;
;         if (sidx < NCH) {
;             const int c = sidx;
;             if (LOCAL && c < 8) {
; #pragma unroll
;                 for (int t2 = 0; t2 < 2; ++t2) {
;                     const LAS bf16* kp = cb + (kc0 + 16 * t2 + fr) * 72 + 8 * fq;
;                     f32x4 acc = {0.f, 0.f, 0.f, 0.f};
;                     acc = __builtin_amdgcn_mfma_f32_16x16x32_bf16(*(const LAS bf16x8*)(kp), qf[0], acc, 0, 0, 0);
;                     acc = __builtin_amdgcn_mfma_f32_16x16x32_bf16(*(const LAS bf16x8*)(kp + 32), qf[1], acc, 0, 0, 0);
;                     const LAS float* rb = rpb + (r0 + c - gr + 7) * 31 + 15 - qcol;
; #pragma unroll
;                     for (int e = 0; e < 4; ++e) { const int kcol = kc0 + 16 * t2 + 4 * fq + e; const bool ok = (kcol >= cs) && (kcol < cs + 16);
;                         const float sv = ok ? acc[e] * 0.125f + rb[ok ? kcol : qcol] : -1.0e30f; acc[e] = sv; m = fmaxf(m, sv); }
;                     sl[2 * (c < 8 ? c : 0) + t2] = acc; }
;             } else {
;                 const int cc = c - NLOC;
; #pragma unroll
;                 for (int t4 = 0; t4 < 4; ++t4) {
;                     const LAS bf16* kp = cb + (16 * t4 + fr) * 72 + 8 * fq;
;                     f32x4 acc = {0.f, 0.f, 0.f, 0.f};
;                     acc = __builtin_amdgcn_mfma_f32_16x16x32_bf16(*(const LAS bf16x8*)(kp), qf[0], acc, 0, 0, 0);
;                     acc = __builtin_amdgcn_mfma_f32_16x16x32_bf16(*(const LAS bf16x8*)(kp + 32), qf[1], acc, 0, 0, 0);
; #pragma unroll
;                     for (int e = 0; e < 4; ++e) { acc[e] *= 0.125f; m = fmaxf(m, acc[e]); }
;                     sc[4 * (cc >= 0 ? cc : 0) + t4] = acc; }
;             }
;             if (sidx == NCH - 1) { m = fmaxf(m, __shfl_xor(m, 16)); m = fmaxf(m, __shfl_xor(m, 32)); }
	ds_read_b32 v240, v31 offset:38660
	ds_read_b32 v241, v31 offset:38664
	ds_read_b32 v242, v31 offset:38668
	ds_read_b32 v243, v31 offset:38672
	ds_read_b32 v244, v31 offset:38724
	ds_read_b32 v245, v31 offset:38728
	ds_read_b32 v246, v31 offset:38732
	ds_read_b32 v247, v31 offset:38736
	ds_read_b128 v[18:21], v32 offset:18432
	ds_read_b128 v[26:29], v32 offset:18496
	v_or_b32_e32 v24, 64, v34
	v_mov_b64_e32 v[22:23], s[8:9]
	v_mad_i64_i32 v[22:23], s[52:53], v24, s72, v[22:23]
	v_lshl_add_u64 v[22:23], v[22:23], 0, v[70:71]
	v_lshl_add_u64 v[22:23], v[22:23], 0, s[2:3]
	s_waitcnt lgkmcnt(1)
	v_mfma_f32_16x16x32_bf16 v[36:39], v[18:21], v[6:9], 0
	v_lshl_add_u64 v[248:249], v[22:23], 0, s[100:101]
	global_load_dwordx4 v[18:21], v[22:23], off offset:1024
	s_nop 0
	global_load_dwordx4 v[22:25], v[22:23], off offset:1152
	global_load_dword v250, v[248:249], off offset:1024
	global_load_dword v251, v[248:249], off offset:1152
	v_mov_b32_e32 v149, 0xf149f2ca
	v_mov_b32_e32 v150, 0xf149f2ca
	s_waitcnt lgkmcnt(0)
	v_mfma_f32_16x16x32_bf16 v[26:29], v[26:29], v[2:5], v[36:39]
	s_nop 2
	s_waitcnt lgkmcnt(0)
	s_nop 3
	v_fmac_f32_e32 v240, 0x3e000000, v26
	v_cndmask_b32_e64 v150, v150, v240, s[28:29]
	s_nop 2
	s_waitcnt lgkmcnt(0)
	s_nop 0
	v_fmac_f32_e32 v241, 0x3e000000, v27
	v_cndmask_b32_e64 v149, v149, v241, s[30:31]
	v_mov_b32_e32 v152, 0xf149f2ca
	v_mov_b32_e32 v153, 0xf149f2ca
	s_nop 2
	s_waitcnt lgkmcnt(0)
	v_fmac_f32_e32 v242, 0x3e000000, v28
	v_cndmask_b32_e64 v153, v153, v242, s[34:35]
	s_nop 2
	s_waitcnt lgkmcnt(0)
	v_fmac_f32_e32 v243, 0x3e000000, v29
	v_cndmask_b32_e64 v152, v152, v243, s[36:37]
	ds_read_b128 v[26:29], v33 offset:18432
	ds_read_b128 v[36:39], v33 offset:18496
	v_mov_b32_e32 v154, 0xf149f2ca
	v_mov_b32_e32 v156, 0xf149f2ca
	s_waitcnt lgkmcnt(1)
	v_mfma_f32_16x16x32_bf16 v[26:29], v[26:29], v[6:9], 0
	s_waitcnt lgkmcnt(0)
	v_mfma_f32_16x16x32_bf16 v[26:29], v[36:39], v[2:5], v[26:29]
	s_nop 2
	s_waitcnt lgkmcnt(0)
	s_nop 3
	v_fmac_f32_e32 v244, 0x3e000000, v26
	v_cndmask_b32_e64 v156, v156, v244, s[38:39]
	s_nop 2
	s_waitcnt lgkmcnt(0)
	s_nop 0
	v_fmac_f32_e32 v245, 0x3e000000, v27
	v_cndmask_b32_e64 v154, v154, v245, s[44:45]
	v_mov_b32_e32 v155, 0xf149f2ca
	v_mov_b32_e32 v158, 0xf149f2ca
	s_nop 2
	s_waitcnt lgkmcnt(0)
	v_fmac_f32_e32 v246, 0x3e000000, v28
	v_cndmask_b32_e64 v158, v158, v246, s[46:47]
	s_nop 2
	s_waitcnt lgkmcnt(0)
	v_fmac_f32_e32 v247, 0x3e000000, v29
	v_cndmask_b32_e64 v155, v155, v247, s[66:67]
	v_max3_f32 v26, v93, s75, v92
	v_max3_f32 v26, v26, v95, v94
	v_max3_f32 v26, v26, v97, v96
	v_max3_f32 v26, v26, v100, v98
	v_max3_f32 v26, v26, v101, v99
	v_max3_f32 v26, v26, v103, v102
	v_max3_f32 v26, v26, v106, v104
	v_max3_f32 v26, v26, v110, v108
	v_max3_f32 v26, v26, v107, v105
	v_max3_f32 v26, v26, v111, v109
	v_max3_f32 v26, v26, v114, v112
	v_max3_f32 v26, v26, v117, v113
	v_max3_f32 v26, v26, v116, v115
	v_max3_f32 v26, v26, v119, v118
	v_max3_f32 v26, v26, v122, v120
	v_max3_f32 v26, v26, v125, v121
	v_max3_f32 v26, v26, v124, v123
	v_max3_f32 v26, v26, v127, v126
	v_max3_f32 v26, v26, v130, v128
	v_max3_f32 v26, v26, v134, v129
	v_max3_f32 v26, v26, v132, v131
	v_max3_f32 v26, v26, v136, v135
	v_max3_f32 v26, v26, v140, v138
	v_max3_f32 v26, v26, v143, v139
	v_max3_f32 v26, v26, v142, v141
	v_max3_f32 v26, v26, v145, v144
	v_mad_u32_u24 v90, v90, s73, v30
	v_max3_f32 v26, v26, v148, v146
	s_waitcnt vmcnt(7)
	ds_write_b128 v75, v[10:13]
	s_waitcnt vmcnt(6)
	ds_write_b128 v75, v[14:17] offset:9216
	s_waitcnt lgkmcnt(0)
	s_barrier
	ds_read_b128 v[10:13], v90
	ds_read_b128 v[14:17], v90 offset:64
	v_max3_f32 v26, v26, v151, v147
	v_max3_f32 v26, v26, v150, v149
	v_max3_f32 v26, v26, v153, v152
	v_max3_f32 v26, v26, v156, v154
	v_max3_f32 v35, v26, v158, v155
	v_or_b32_e32 v26, 0x80, v34
	v_mov_b64_e32 v[44:45], s[8:9]
	v_mad_i64_i32 v[26:27], s[28:29], v26, s72, v[44:45]
	v_lshl_add_u64 v[26:27], v[26:27], 0, v[70:71]
	v_lshl_add_u64 v[30:31], v[26:27], 0, s[2:3]
	s_waitcnt lgkmcnt(1)
	v_mfma_f32_16x16x32_bf16 v[10:13], v[10:13], v[6:9], 0
	v_lshl_add_u64 v[248:249], v[30:31], 0, s[100:101]
	global_load_dwordx4 v[26:29], v[30:31], off offset:1024
	s_nop 0
	global_load_dwordx4 v[30:33], v[30:31], off offset:1152
	global_load_dword v250, v[248:249], off offset:1024
	global_load_dword v251, v[248:249], off offset:1152
	ds_read_b128 v[36:39], v90 offset:2304
	v_lshl_add_u64 v[78:79], s[4:5], 0, v[70:71]
	s_waitcnt lgkmcnt(1)
	v_mfma_f32_16x16x32_bf16 v[62:65], v[14:17], v[2:5], v[10:13]
	s_ashr_i32 s17, s16, 31
	v_mov_b32_e32 v81, v71
	v_cmp_lt_i32_e32 vcc, v84, v85
	ds_read_b128 v[10:13], v90 offset:2368
	v_add3_u32 v157, v87, v76, v88
	s_nop 2
	v_mul_f32_e32 v14, 0x3e000000, v62
	v_mul_f32_e32 v15, 0x3e000000, v63
	v_max3_f32 v35, v35, v14, v15
	v_mul_f32_e32 v40, 0x3e000000, v64
	s_waitcnt lgkmcnt(1)
	v_mfma_f32_16x16x32_bf16 v[14:17], v[36:39], v[6:9], 0
	v_mul_f32_e32 v36, 0x3e000000, v65
	v_max3_f32 v35, v35, v40, v36
	ds_read_b128 v[36:39], v90 offset:4608
	s_waitcnt lgkmcnt(1)
	v_mfma_f32_16x16x32_bf16 v[66:69], v[10:13], v[2:5], v[14:17]
	ds_read_b128 v[10:13], v90 offset:4672
	s_ashr_i32 s19, s18, 31
	s_ashr_i32 s21, s20, 31
	s_ashr_i32 s23, s22, 31
	s_ashr_i32 s25, s24, 31
	s_nop 2
	v_mul_f32_e32 v14, 0x3e000000, v66
	v_mul_f32_e32 v15, 0x3e000000, v67
	v_max3_f32 v35, v35, v14, v15
	s_waitcnt lgkmcnt(1)
	v_mfma_f32_16x16x32_bf16 v[14:17], v[36:39], v[6:9], 0
	v_mul_f32_e32 v40, 0x3e000000, v68
	v_mul_f32_e32 v41, 0x3e000000, v69
	v_max3_f32 v35, v35, v40, v41
	s_waitcnt lgkmcnt(0)
	v_mfma_f32_16x16x32_bf16 v[58:61], v[10:13], v[2:5], v[14:17]
	ds_read_b128 v[36:39], v90 offset:6912
	ds_read_b128 v[40:43], v90 offset:6976
	s_waitcnt vmcnt(7)
	ds_write_b128 v75, v[18:21] offset:18432
	s_waitcnt vmcnt(6)
	ds_write_b128 v75, v[22:25] offset:27648
	s_waitcnt lgkmcnt(0)
	s_nop 0
	v_mul_f32_e32 v10, 0x3e000000, v58
	v_mul_f32_e32 v11, 0x3e000000, v59
	v_max3_f32 v14, v35, v10, v11
	v_mfma_f32_16x16x32_bf16 v[10:13], v[36:39], v[6:9], 0
	v_mul_f32_e32 v15, 0x3e000000, v60
	v_mul_f32_e32 v16, 0x3e000000, v61
	v_max3_f32 v14, v14, v15, v16
	v_mfma_f32_16x16x32_bf16 v[54:57], v[40:43], v[2:5], v[10:13]
	s_barrier
; #define LAS __attribute__((address_space(3)))
; template <bool LOCAL>
; __device__ __forceinline__ void na_unit(const bf16* P, const bf16* VT, bf16* YCAT, const LAS float* rpb_l, LAS bf16* buf, int b, int gr, int hp, int qblk, int tid) {
;     ...
;                 const int cc = c - NLOC;
; #pragma unroll
;                 for (int t4 = 0; t4 < 4; ++t4) {
;                     const LAS bf16* kp = cb + (16 * t4 + fr) * 72 + 8 * fq;
;                     f32x4 acc = {0.f, 0.f, 0.f, 0.f};
;                     acc = __builtin_amdgcn_mfma_f32_16x16x32_bf16(*(const LAS bf16x8*)(kp), qf[0], acc, 0, 0, 0);
;                     acc = __builtin_amdgcn_mfma_f32_16x16x32_bf16(*(const LAS bf16x8*)(kp + 32), qf[1], acc, 0, 0, 0);
; #pragma unroll
;                     for (int e = 0; e < 4; ++e) { acc[e] *= 0.125f; m = fmaxf(m, acc[e]); }
;                     sc[4 * (cc >= 0 ? cc : 0) + t4] = acc; }
;             }
;             if (sidx == NCH - 1) { m = fmaxf(m, __shfl_xor(m, 16)); m = fmaxf(m, __shfl_xor(m, 32)); }
	v_or_b32_e32 v18, 0xc0, v34
	v_mad_i64_i32 v[18:19], s[28:29], v18, s72, v[44:45]
	v_lshl_add_u64 v[18:19], v[18:19], 0, v[70:71]
	s_nop 3
	v_mul_f32_e32 v10, 0x3e000000, v54
	v_mul_f32_e32 v11, 0x3e000000, v55
	v_max3_f32 v14, v14, v10, v11
	ds_read_b128 v[10:13], v90 offset:18432
	v_mul_f32_e32 v15, 0x3e000000, v56
	v_mul_f32_e32 v16, 0x3e000000, v57
	v_max3_f32 v35, v14, v15, v16
	ds_read_b128 v[14:17], v90 offset:18496
	v_lshl_add_u64 v[22:23], v[18:19], 0, s[2:3]
	s_waitcnt lgkmcnt(1)
	v_mfma_f32_16x16x32_bf16 v[10:13], v[10:13], v[6:9], 0
	global_load_dwordx4 v[18:21], v[22:23], off offset:1024
	global_load_dwordx4 v[160:163], v[22:23], off offset:1152
	ds_read_b128 v[22:25], v90 offset:20736
	s_ashr_i32 s27, s26, 31
	s_waitcnt lgkmcnt(1)
	v_mfma_f32_16x16x32_bf16 v[46:49], v[14:17], v[2:5], v[10:13]
	s_nop 2
	ds_read_b128 v[10:13], v90 offset:20800
	s_nop 3
	v_mul_f32_e32 v14, 0x3e000000, v46
	v_mul_f32_e32 v15, 0x3e000000, v47
	v_max3_f32 v34, v35, v14, v15
	v_mul_f32_e32 v35, 0x3e000000, v48
	s_waitcnt lgkmcnt(1)
	v_mfma_f32_16x16x32_bf16 v[14:17], v[22:25], v[6:9], 0
	v_mul_f32_e32 v22, 0x3e000000, v49
	v_max3_f32 v34, v34, v35, v22
	ds_read_b128 v[22:25], v90 offset:23040
	s_waitcnt lgkmcnt(1)
	v_mfma_f32_16x16x32_bf16 v[50:53], v[10:13], v[2:5], v[14:17]
	ds_read_b128 v[10:13], v90 offset:23104
	s_nop 6
	v_mul_f32_e32 v14, 0x3e000000, v50
	v_mul_f32_e32 v15, 0x3e000000, v51
	v_max3_f32 v34, v34, v14, v15
	s_waitcnt lgkmcnt(1)
	v_mfma_f32_16x16x32_bf16 v[14:17], v[22:25], v[6:9], 0
	v_mul_f32_e32 v35, 0x3e000000, v52
	v_mul_f32_e32 v36, 0x3e000000, v53
	v_max3_f32 v38, v34, v35, v36
	s_waitcnt lgkmcnt(0)
	v_mfma_f32_16x16x32_bf16 v[42:45], v[10:13], v[2:5], v[14:17]
	ds_read_b128 v[22:25], v90 offset:25344
	ds_read_b128 v[34:37], v90 offset:25408
	s_waitcnt vmcnt(5)
	ds_write_b128 v75, v[26:29]
	s_waitcnt vmcnt(4)
	ds_write_b128 v75, v[30:33] offset:9216
	s_waitcnt lgkmcnt(0)
	s_nop 0
	v_mul_f32_e32 v10, 0x3e000000, v42
	v_mul_f32_e32 v11, 0x3e000000, v43
	v_max3_f32 v14, v38, v10, v11
	v_mfma_f32_16x16x32_bf16 v[10:13], v[22:25], v[6:9], 0
	v_mul_f32_e32 v15, 0x3e000000, v44
	v_mul_f32_e32 v16, 0x3e000000, v45
	v_max3_f32 v14, v14, v15, v16
	v_mfma_f32_16x16x32_bf16 v[38:41], v[34:37], v[2:5], v[10:13]
	s_barrier
	v_add3_u32 v26, v89, s1, 64
	v_mul_u32_u24_e32 v26, 0x9000, v26
	v_lshl_add_u64 v[22:23], s[16:17], 1, v[78:79]
	s_nop 3
	v_mul_f32_e32 v10, 0x3e000000, v38
	v_mul_f32_e32 v11, 0x3e000000, v39
	v_max3_f32 v10, v14, v10, v11
	v_mul_f32_e32 v11, 0x3e000000, v40
	v_mul_f32_e32 v12, 0x3e000000, v41
	v_max3_f32 v34, v10, v11, v12
	v_or_b32_e32 v10, s1, v89
	v_mul_u32_u24_e32 v14, 0x9000, v10
	ds_read_b128 v[10:13], v90
	v_lshlrev_b32_e32 v70, 1, v14
	ds_read_b128 v[14:17], v90 offset:64
	v_lshlrev_b32_e32 v80, 1, v26
	v_lshl_add_u64 v[24:25], v[22:23], 0, v[70:71]
	v_lshl_add_u64 v[22:23], v[22:23], 0, v[80:81]
	s_waitcnt lgkmcnt(1)
	v_mfma_f32_16x16x32_bf16 v[10:13], v[10:13], v[6:9], 0
	v_lshl_add_u64 v[248:249], v[24:25], 0, 0
	v_lshl_add_u64 v[238:239], v[22:23], 0, 0
	global_load_dwordx4 v[164:167], v[24:25], off
	global_load_dwordx4 v[172:175], v[22:23], off
	global_load_dword v250, v[248:249], off offset:128
	global_load_dword v251, v[238:239], off offset:128
	ds_read_b128 v[22:25], v90 offset:2304
	s_add_i32 s16, s15, s50
	s_waitcnt lgkmcnt(1)
	v_mfma_f32_16x16x32_bf16 v[30:33], v[14:17], v[2:5], v[10:13]
	s_ashr_i32 s17, s16, 31
	s_ashr_i32 s15, s14, 31
	v_lshl_add_u64 v[168:169], s[14:15], 1, v[78:79]
	ds_read_b128 v[10:13], v90 offset:2368
	s_ashr_i32 s1, s0, 31
	s_nop 2
	v_mul_f32_e32 v14, 0x3e000000, v30
	v_mul_f32_e32 v15, 0x3e000000, v31
	v_max3_f32 v26, v34, v14, v15
	v_mul_f32_e32 v27, 0x3e000000, v32
	s_waitcnt lgkmcnt(1)
	v_mfma_f32_16x16x32_bf16 v[14:17], v[22:25], v[6:9], 0
	v_mul_f32_e32 v22, 0x3e000000, v33
	v_max3_f32 v26, v26, v27, v22
	ds_read_b128 v[22:25], v90 offset:4608
	s_waitcnt lgkmcnt(1)
	v_mfma_f32_16x16x32_bf16 v[34:37], v[10:13], v[2:5], v[14:17]
	ds_read_b128 v[10:13], v90 offset:4672
	s_nop 6
	v_mul_f32_e32 v14, 0x3e000000, v34
	v_mul_f32_e32 v15, 0x3e000000, v35
	v_max3_f32 v26, v26, v14, v15
	s_waitcnt lgkmcnt(1)
	v_mfma_f32_16x16x32_bf16 v[14:17], v[22:25], v[6:9], 0
	v_mul_f32_e32 v27, 0x3e000000, v36
	v_mul_f32_e32 v28, 0x3e000000, v37
	v_max3_f32 v89, v26, v27, v28
	s_waitcnt lgkmcnt(0)
	v_mfma_f32_16x16x32_bf16 v[26:29], v[10:13], v[2:5], v[14:17]
	ds_read_b128 v[22:25], v90 offset:6912
	ds_read_b128 v[176:179], v90 offset:6976
	s_waitcnt vmcnt(5)
	ds_write_b128 v75, v[18:21] offset:18432
	s_waitcnt vmcnt(4)
	ds_write_b128 v75, v[160:163] offset:27648
	s_waitcnt lgkmcnt(0)
	s_nop 0
	v_mul_f32_e32 v10, 0x3e000000, v26
	v_mul_f32_e32 v11, 0x3e000000, v27
	v_max3_f32 v14, v89, v10, v11
	v_mfma_f32_16x16x32_bf16 v[10:13], v[22:25], v[6:9], 0
	v_mul_f32_e32 v15, 0x3e000000, v28
	v_mul_f32_e32 v16, 0x3e000000, v29
	v_max3_f32 v14, v14, v15, v16
	v_mfma_f32_16x16x32_bf16 v[22:25], v[176:179], v[2:5], v[10:13]
	s_barrier
; #define LAS __attribute__((address_space(3)))
; __device__ __forceinline__ unsigned cvt_pk_bf16(float lo, float hi) { const float __attribute__((ext_vector_type(2))) v = {lo, hi}; return __builtin_bit_cast(unsigned, __builtin_convertvector(v, bf16x2_t)); }
; template <bool LOCAL>
; __device__ __forceinline__ void na_unit(const bf16* P, const bf16* VT, bf16* YCAT, const LAS float* rpb_l, LAS bf16* buf, int b, int gr, int hp, int qblk, int tid) {
;     ...
;             if (sidx == NCH - 1) { m = fmaxf(m, __shfl_xor(m, 16)); m = fmaxf(m, __shfl_xor(m, 32)); }
;         } else {
;             const int c = sidx - NCH;
;             if (LOCAL && c < 8) {
;                 float p[8];
; #pragma unroll
;                 for (int e = 0; e < 4; ++e) { p[e] = __expf(sl[2 * (c < 8 ? c : 0)][e] - m); p[4 + e] = __expf(sl[2 * (c < 8 ? c : 0) + 1][e] - m); }
; #pragma unroll
;                 for (int e = 0; e < 8; ++e) lsum += p[e];
;                 const bf16x8 pf = __builtin_bit_cast(bf16x8, (v4u){pg8::cvt_pk_bf16(p[0], p[1]), pg8::cvt_pk_bf16(p[2], p[3]), pg8::cvt_pk_bf16(p[4], p[5]), pg8::cvt_pk_bf16(p[6], p[7])});
; #pragma unroll
;                 for (int dt = 0; dt < 4; ++dt) { const LAS bf16* vp = cb + (16 * dt + fr) * 72 + kc0 + 4 * fq;
;                     o[dt] = __builtin_amdgcn_mfma_f32_16x16x32_bf16(frag44(vp, vp + 16), pf, o[dt], 0, 0, 0); }
	v_lshl_add_u64 v[18:19], s[16:17], 1, v[78:79]
	v_lshl_add_u64 v[20:21], v[18:19], 0, v[70:71]
	v_lshl_add_u64 v[18:19], v[18:19], 0, v[80:81]
	s_nop 3
	v_mul_f32_e32 v10, 0x3e000000, v22
	v_mul_f32_e32 v11, 0x3e000000, v23
	v_max3_f32 v14, v14, v10, v11
	ds_read_b128 v[10:13], v90 offset:18432
	v_mul_f32_e32 v15, 0x3e000000, v24
	v_mul_f32_e32 v16, 0x3e000000, v25
	v_max3_f32 v89, v14, v15, v16
	ds_read_b128 v[14:17], v90 offset:18496
	s_waitcnt lgkmcnt(1)
	v_mfma_f32_16x16x32_bf16 v[10:13], v[10:13], v[6:9], 0
	v_lshl_add_u64 v[248:249], v[20:21], 0, 0
	v_lshl_add_u64 v[238:239], v[18:19], 0, 0
	global_load_dwordx4 v[160:163], v[20:21], off
	global_load_dwordx4 v[176:179], v[18:19], off
	global_load_dword v250, v[248:249], off offset:128
	global_load_dword v251, v[238:239], off offset:128
	ds_read_b128 v[18:21], v90 offset:20736
	ds_read_b128 v[180:183], v90 offset:23040
	s_waitcnt lgkmcnt(2)
	v_mfma_f32_16x16x32_bf16 v[14:17], v[14:17], v[2:5], v[10:13]
	s_nop 2
	ds_read_b128 v[10:13], v90 offset:20800
	s_waitcnt lgkmcnt(2)
	v_mfma_f32_16x16x32_bf16 v[18:21], v[18:21], v[6:9], 0
	s_nop 1
	v_mul_f32_e32 v133, 0x3e000000, v14
	v_mul_f32_e32 v137, 0x3e000000, v15
	v_max3_f32 v89, v89, v133, v137
	s_waitcnt lgkmcnt(0)
	v_mfma_f32_16x16x32_bf16 v[18:21], v[10:13], v[2:5], v[18:21]
	ds_read_b128 v[10:13], v90 offset:23104
	ds_read_b128 v[184:187], v90 offset:25344
	ds_read_b128 v[188:191], v90 offset:25408
	v_mul_f32_e32 v133, 0x3e000000, v16
	v_mfma_f32_16x16x32_bf16 v[180:183], v[180:183], v[6:9], 0
	v_mul_f32_e32 v137, 0x3e000000, v17
	v_max3_f32 v89, v89, v133, v137
	s_nop 0
	v_mul_f32_e32 v133, 0x3e000000, v18
	s_waitcnt lgkmcnt(1)
	v_mfma_f32_16x16x32_bf16 v[6:9], v[184:187], v[6:9], 0
	v_mul_f32_e32 v137, 0x3e000000, v19
	v_max3_f32 v89, v89, v133, v137
	v_mul_f32_e32 v133, 0x3e000000, v20
	v_mfma_f32_16x16x32_bf16 v[10:13], v[10:13], v[2:5], v[180:183]
	v_mul_f32_e32 v137, 0x3e000000, v21
	v_max3_f32 v89, v89, v133, v137
	s_waitcnt vmcnt(7)
	ds_write_b128 v75, v[164:167]
	s_waitcnt vmcnt(6)
	ds_write_b128 v75, v[172:175] offset:9216
	s_waitcnt lgkmcnt(2)
	v_mfma_f32_16x16x32_bf16 v[2:5], v[188:191], v[2:5], v[6:9]
	v_mul_f32_e32 v90, 0x3e000000, v10
	v_mul_f32_e32 v133, 0x3e000000, v11
	v_max3_f32 v89, v89, v90, v133
	v_mul_f32_e32 v90, 0x3e000000, v12
	v_mul_f32_e32 v133, 0x3e000000, v13
	v_max3_f32 v89, v89, v90, v133
	s_nop 1
	v_mul_f32_e32 v6, 0x3e000000, v2
	v_mul_f32_e32 v7, 0x3e000000, v3
	v_max3_f32 v6, v89, v6, v7
	v_mul_f32_e32 v7, 0x3e000000, v4
	v_mul_f32_e32 v8, 0x3e000000, v5
	v_max3_f32 v6, v6, v7, v8
	v_cndmask_b32_e32 v7, v83, v84, vcc
	v_lshlrev_b32_e32 v89, 2, v7
	ds_bpermute_b32 v7, v89, v6
	v_cmp_lt_i32_e32 vcc, v86, v85
	v_lshl_add_u32 v8, v91, 1, v157
	v_lshl_add_u64 v[188:189], v[168:169], 0, v[70:71]
	s_waitcnt lgkmcnt(0)
	v_max_f32_e32 v7, v7, v7
	v_max_f32_e32 v6, v6, v7
	v_cndmask_b32_e32 v7, v83, v86, vcc
	v_lshlrev_b32_e32 v90, 2, v7
	ds_bpermute_b32 v7, v90, v6
	s_barrier
	s_waitcnt lgkmcnt(0)
	ds_read2_b64 v[164:167], v8 offset1:4
	v_lshl_add_u64 v[168:169], v[168:169], 0, v[80:81]
	v_max_f32_e32 v7, v7, v7
	v_max_f32_e32 v137, v6, v7
	v_sub_f32_e32 v6, v93, v137
	v_mul_f32_e32 v6, 0x3fb8aa3b, v6
	v_exp_f32_e32 v133, v6
	v_sub_f32_e32 v6, v97, v137
	v_mul_f32_e32 v6, 0x3fb8aa3b, v6
	v_exp_f32_e32 v93, v6
	v_sub_f32_e32 v6, v92, v137
	v_mul_f32_e32 v6, 0x3fb8aa3b, v6
	v_exp_f32_e32 v97, v6
	v_sub_f32_e32 v6, v96, v137
	v_mul_f32_e32 v6, 0x3fb8aa3b, v6
	v_exp_f32_e32 v92, v6
	v_sub_f32_e32 v6, v95, v137
	v_mul_f32_e32 v6, 0x3fb8aa3b, v6
	v_exp_f32_e32 v96, v6
	v_sub_f32_e32 v6, v100, v137
	v_mul_f32_e32 v6, 0x3fb8aa3b, v6
	v_exp_f32_e32 v95, v6
	v_sub_f32_e32 v6, v94, v137
	v_mul_f32_e32 v6, 0x3fb8aa3b, v6
	v_exp_f32_e32 v100, v6
	v_sub_f32_e32 v6, v98, v137
	v_mul_f32_e32 v6, 0x3fb8aa3b, v6
	v_exp_f32_e32 v94, v6
	v_add_u32_e32 v7, 0x800, v8
	v_add_u32_e32 v6, 0x1000, v8
	ds_read2_b64 v[180:183], v7 offset0:32 offset1:36
	ds_read2_b64 v[184:187], v6 offset0:64 offset1:68
	v_lshl_add_u64 v[248:249], v[188:189], 0, 0
	v_lshl_add_u64 v[238:239], v[168:169], 0, 0
	global_load_dwordx4 v[188:191], v[188:189], off
	s_nop 0
	global_load_dwordx4 v[192:195], v[168:169], off
	global_load_dword v250, v[248:249], off offset:128
	global_load_dword v251, v[238:239], off offset:128
	v_sub_f32_e32 v9, v101, v137
	v_mul_f32_e32 v9, 0x3fb8aa3b, v9
	v_add_u32_e32 v159, 0x1800, v8
	v_exp_f32_e32 v87, v9
	v_sub_f32_e32 v9, v106, v137
	ds_read2_b64 v[196:199], v159 offset0:96 offset1:100
	v_mul_f32_e32 v9, 0x3fb8aa3b, v9
	v_exp_f32_e32 v76, v9
	v_sub_f32_e32 v9, v99, v137
	v_mul_f32_e32 v9, 0x3fb8aa3b, v9
	v_exp_f32_e32 v91, v9
	v_sub_f32_e32 v9, v104, v137
	v_mul_f32_e32 v9, 0x3fb8aa3b, v9
	v_exp_f32_e32 v88, v9
	v_sub_f32_e32 v9, v103, v137
	v_mul_f32_e32 v9, 0x3fb8aa3b, v9
	v_exp_f32_e32 v99, v9
	v_sub_f32_e32 v9, v110, v137
	v_cvt_pk_bf16_f32 v172, v133, v97
	v_cvt_pk_bf16_f32 v173, v96, v100
	v_cvt_pk_bf16_f32 v174, v93, v92
	v_cvt_pk_bf16_f32 v175, v95, v94
	s_waitcnt vmcnt(7)
	ds_write_b128 v75, v[160:163] offset:18432
	s_waitcnt vmcnt(6)
	ds_write_b128 v75, v[176:179] offset:27648
	v_mul_f32_e32 v9, 0x3fb8aa3b, v9
	v_add_u32_e32 v161, 0x4800, v8
	v_add_u32_e32 v160, 0x5000, v8
	s_waitcnt lgkmcnt(5)
	v_mfma_f32_16x16x32_bf16 v[164:167], v[164:167], v[172:175], 0
	s_waitcnt lgkmcnt(0)
	s_barrier
; #define LAS __attribute__((address_space(3)))
; __device__ __forceinline__ unsigned cvt_pk_bf16(float lo, float hi) { const float __attribute__((ext_vector_type(2))) v = {lo, hi}; return __builtin_bit_cast(unsigned, __builtin_convertvector(v, bf16x2_t)); }
; template <bool LOCAL>
; __device__ __forceinline__ void na_unit(const bf16* P, const bf16* VT, bf16* YCAT, const LAS float* rpb_l, LAS bf16* buf, int b, int gr, int hp, int qblk, int tid) {
;     ...
;             const int c = sidx - NCH;
;             if (LOCAL && c < 8) {
;                 float p[8];
; #pragma unroll
;                 for (int e = 0; e < 4; ++e) { p[e] = __expf(sl[2 * (c < 8 ? c : 0)][e] - m); p[4 + e] = __expf(sl[2 * (c < 8 ? c : 0) + 1][e] - m); }
; #pragma unroll
;                 for (int e = 0; e < 8; ++e) lsum += p[e];
;                 const bf16x8 pf = __builtin_bit_cast(bf16x8, (v4u){pg8::cvt_pk_bf16(p[0], p[1]), pg8::cvt_pk_bf16(p[2], p[3]), pg8::cvt_pk_bf16(p[4], p[5]), pg8::cvt_pk_bf16(p[6], p[7])});
; #pragma unroll
;                 for (int dt = 0; dt < 4; ++dt) { const LAS bf16* vp = cb + (16 * dt + fr) * 72 + kc0 + 4 * fq;
;                     o[dt] = __builtin_amdgcn_mfma_f32_16x16x32_bf16(frag44(vp, vp + 16), pf, o[dt], 0, 0, 0); }
;             } else {
;                 const int cc = c - NLOC;
; #pragma unroll
;                 for (int p2 = 0; p2 < 2; ++p2) {
;                     float p[8];
; #pragma unroll
;                     for (int e = 0; e < 4; ++e) { p[e] = __expf(sc[4 * (cc >= 0 ? cc : 0) + 2 * p2][e] - m); p[4 + e] = __expf(sc[4 * (cc >= 0 ? cc : 0) + 2 * p2 + 1][e] - m); }
; #pragma unroll
;                     for (int e = 0; e < 8; ++e) lsum += p[e];
;                     const bf16x8 pf = __builtin_bit_cast(bf16x8, (v4u){pg8::cvt_pk_bf16(p[0], p[1]), pg8::cvt_pk_bf16(p[2], p[3]), pg8::cvt_pk_bf16(p[4], p[5]), pg8::cvt_pk_bf16(p[6], p[7])});
; #pragma unroll
;                     for (int dt = 0; dt < 4; ++dt) { const LAS bf16* vp = cb + (16 * dt + fr) * 72 + 32 * p2 + 4 * fq;
;                         o[dt] = __builtin_amdgcn_mfma_f32_16x16x32_bf16(frag44(vp, vp + 16), pf, o[dt], 0, 0, 0); }
;                 }
;             }
;         }
;         if (sidx + 1 < 2 * NCH) NA_STORE(sidx + 1);
	v_mfma_f32_16x16x32_bf16 v[180:183], v[180:183], v[172:175], 0
	v_exp_f32_e32 v98, v9
	v_sub_f32_e32 v9, v102, v137
	ds_read2_b64 v[176:179], v161 offset1:4
	v_mfma_f32_16x16x32_bf16 v[184:187], v[184:187], v[172:175], 0
	v_mul_f32_e32 v9, 0x3fb8aa3b, v9
	v_exp_f32_e32 v101, v9
	v_sub_f32_e32 v9, v108, v137
	v_mfma_f32_16x16x32_bf16 v[172:175], v[196:199], v[172:175], 0
	ds_read2_b64 v[196:199], v160 offset0:32 offset1:36
	v_mul_f32_e32 v9, 0x3fb8aa3b, v9
	v_exp_f32_e32 v102, v9
	v_lshl_add_u64 v[162:163], s[0:1], 1, v[78:79]
	v_cvt_pk_bf16_f32 v200, v87, v91
	v_cvt_pk_bf16_f32 v201, v99, v101
	v_cvt_pk_bf16_f32 v202, v76, v88
	v_cvt_pk_bf16_f32 v203, v98, v102
	v_lshl_add_u64 v[168:169], v[162:163], 0, v[70:71]
	v_lshl_add_u64 v[204:205], v[162:163], 0, v[80:81]
	v_add_u32_e32 v162, 0x5800, v8
	s_waitcnt lgkmcnt(1)
	v_mfma_f32_16x16x32_bf16 v[164:167], v[176:179], v[200:203], v[164:167]
	v_sub_f32_e32 v9, v107, v137
	v_mul_f32_e32 v9, 0x3fb8aa3b, v9
	v_add_u32_e32 v163, 0x6000, v8
	s_waitcnt lgkmcnt(0)
	v_mfma_f32_16x16x32_bf16 v[176:179], v[196:199], v[200:203], v[180:183]
	v_exp_f32_e32 v104, v9
	v_sub_f32_e32 v9, v114, v137
	v_mul_f32_e32 v9, 0x3fb8aa3b, v9
	ds_read2_b64 v[180:183], v162 offset0:64 offset1:68
	v_lshl_add_u64 v[248:249], v[168:169], 0, 0
	v_lshl_add_u64 v[238:239], v[204:205], 0, 0
	global_load_dwordx4 v[196:199], v[168:169], off
	s_nop 0
	global_load_dwordx4 v[204:207], v[204:205], off
	global_load_dword v250, v[248:249], off offset:128
	global_load_dword v251, v[238:239], off offset:128
	s_waitcnt lgkmcnt(0)
	v_mfma_f32_16x16x32_bf16 v[180:183], v[180:183], v[200:203], v[184:187]
	s_nop 2
	ds_read2_b64 v[184:187], v163 offset0:96 offset1:100
	v_exp_f32_e32 v103, v9
	v_sub_f32_e32 v9, v105, v137
	v_mul_f32_e32 v9, 0x3fb8aa3b, v9
	v_exp_f32_e32 v106, v9
	v_sub_f32_e32 v9, v112, v137
	v_mul_f32_e32 v9, 0x3fb8aa3b, v9
	v_exp_f32_e32 v105, v9
	v_sub_f32_e32 v9, v111, v137
	v_mul_f32_e32 v9, 0x3fb8aa3b, v9
	v_exp_f32_e32 v108, v9
	v_sub_f32_e32 v9, v117, v137
	v_mul_f32_e32 v9, 0x3fb8aa3b, v9
	s_waitcnt lgkmcnt(0)
	v_mfma_f32_16x16x32_bf16 v[172:175], v[184:187], v[200:203], v[172:175]
	s_waitcnt vmcnt(7)
	ds_write_b128 v75, v[188:191]
	s_waitcnt vmcnt(6)
	ds_write_b128 v75, v[192:195] offset:9216
	s_waitcnt lgkmcnt(0)
	s_barrier
	v_exp_f32_e32 v107, v9
	v_sub_f32_e32 v9, v109, v137
	ds_read2_b64 v[184:187], v8 offset1:4
	ds_read2_b64 v[188:191], v7 offset0:32 offset1:36
	v_mul_f32_e32 v9, 0x3fb8aa3b, v9
	v_exp_f32_e32 v109, v9
	v_sub_f32_e32 v9, v113, v137
	v_mul_f32_e32 v9, 0x3fb8aa3b, v9
	v_exp_f32_e32 v110, v9
	v_lshl_add_u64 v[168:169], s[18:19], 1, v[78:79]
	v_cvt_pk_bf16_f32 v192, v104, v106
	v_cvt_pk_bf16_f32 v193, v108, v109
	v_cvt_pk_bf16_f32 v194, v103, v105
	v_cvt_pk_bf16_f32 v195, v107, v110
	v_lshl_add_u64 v[112:113], v[168:169], 0, v[70:71]
	v_lshl_add_u64 v[168:169], v[168:169], 0, v[80:81]
	s_waitcnt lgkmcnt(1)
	v_mfma_f32_16x16x32_bf16 v[164:167], v[184:187], v[192:195], v[164:167]
	ds_read2_b64 v[184:187], v6 offset0:64 offset1:68
	v_sub_f32_e32 v9, v116, v137
	v_mul_f32_e32 v9, 0x3fb8aa3b, v9
	s_waitcnt lgkmcnt(1)
	v_mfma_f32_16x16x32_bf16 v[176:179], v[188:191], v[192:195], v[176:179]
	v_lshl_add_u64 v[248:249], v[112:113], 0, 0
	v_lshl_add_u64 v[238:239], v[168:169], 0, 0
	global_load_dwordx4 v[188:191], v[112:113], off
	global_load_dwordx4 v[200:203], v[168:169], off
	global_load_dword v250, v[248:249], off offset:128
	global_load_dword v251, v[238:239], off offset:128
	v_exp_f32_e32 v112, v9
	v_sub_f32_e32 v9, v122, v137
	s_waitcnt lgkmcnt(0)
	v_mfma_f32_16x16x32_bf16 v[180:183], v[184:187], v[192:195], v[180:183]
	ds_read2_b64 v[184:187], v159 offset0:96 offset1:100
	v_mul_f32_e32 v9, 0x3fb8aa3b, v9
	v_exp_f32_e32 v111, v9
	v_sub_f32_e32 v9, v115, v137
	v_mul_f32_e32 v9, 0x3fb8aa3b, v9
	v_exp_f32_e32 v114, v9
	v_sub_f32_e32 v9, v120, v137
	v_mul_f32_e32 v9, 0x3fb8aa3b, v9
	v_exp_f32_e32 v113, v9
	v_sub_f32_e32 v9, v119, v137
	v_mul_f32_e32 v9, 0x3fb8aa3b, v9
	v_exp_f32_e32 v116, v9
	v_sub_f32_e32 v9, v125, v137
	v_mul_f32_e32 v9, 0x3fb8aa3b, v9
	s_waitcnt lgkmcnt(0)
	v_mfma_f32_16x16x32_bf16 v[172:175], v[184:187], v[192:195], v[172:175]
	s_waitcnt vmcnt(7)
	ds_write_b128 v75, v[196:199] offset:18432
	s_waitcnt vmcnt(6)
	ds_write_b128 v75, v[204:207] offset:27648
	s_waitcnt lgkmcnt(0)
	s_barrier
	v_exp_f32_e32 v115, v9
	v_sub_f32_e32 v9, v118, v137
	ds_read2_b64 v[184:187], v161 offset1:4
	v_mul_f32_e32 v9, 0x3fb8aa3b, v9
	v_exp_f32_e32 v117, v9
	v_sub_f32_e32 v9, v121, v137
	v_mul_f32_e32 v9, 0x3fb8aa3b, v9
	v_exp_f32_e32 v118, v9
	v_lshl_add_u64 v[168:169], s[20:21], 1, v[78:79]
	v_lshl_add_u64 v[204:205], v[168:169], 0, v[70:71]
	v_cvt_pk_bf16_f32 v196, v112, v114
	v_cvt_pk_bf16_f32 v197, v116, v117
	v_cvt_pk_bf16_f32 v198, v111, v113
	v_cvt_pk_bf16_f32 v199, v115, v118
	ds_read2_b64 v[192:195], v160 offset0:32 offset1:36
	v_lshl_add_u64 v[120:121], v[168:169], 0, v[80:81]
	s_waitcnt lgkmcnt(1)
	v_mfma_f32_16x16x32_bf16 v[164:167], v[184:187], v[196:199], v[164:167]
	v_lshl_add_u64 v[248:249], v[204:205], 0, 0
	v_lshl_add_u64 v[238:239], v[120:121], 0, 0
	global_load_dwordx4 v[184:187], v[204:205], off
	s_nop 0
	global_load_dwordx4 v[204:207], v[120:121], off
	global_load_dword v250, v[248:249], off offset:128
	global_load_dword v251, v[238:239], off offset:128
	v_sub_f32_e32 v9, v124, v137
	v_mul_f32_e32 v9, 0x3fb8aa3b, v9
	s_waitcnt lgkmcnt(0)
	v_mfma_f32_16x16x32_bf16 v[176:179], v[192:195], v[196:199], v[176:179]
	ds_read2_b64 v[192:195], v162 offset0:64 offset1:68
	v_exp_f32_e32 v120, v9
	v_sub_f32_e32 v9, v130, v137
	s_waitcnt lgkmcnt(0)
	v_mfma_f32_16x16x32_bf16 v[180:183], v[192:195], v[196:199], v[180:183]
	ds_read2_b64 v[192:195], v163 offset0:96 offset1:100
	v_mul_f32_e32 v9, 0x3fb8aa3b, v9
	v_exp_f32_e32 v119, v9
	v_sub_f32_e32 v9, v123, v137
	v_mul_f32_e32 v9, 0x3fb8aa3b, v9
	v_exp_f32_e32 v122, v9
	v_sub_f32_e32 v9, v128, v137
	v_mul_f32_e32 v9, 0x3fb8aa3b, v9
	v_exp_f32_e32 v121, v9
	v_sub_f32_e32 v9, v127, v137
	v_mul_f32_e32 v9, 0x3fb8aa3b, v9
	v_exp_f32_e32 v124, v9
	v_sub_f32_e32 v9, v134, v137
	v_mul_f32_e32 v9, 0x3fb8aa3b, v9
	s_waitcnt lgkmcnt(0)
	v_mfma_f32_16x16x32_bf16 v[172:175], v[192:195], v[196:199], v[172:175]
	s_waitcnt vmcnt(7)
	ds_write_b128 v75, v[188:191]
	s_waitcnt vmcnt(6)
	ds_write_b128 v75, v[200:203] offset:9216
	s_waitcnt lgkmcnt(0)
	s_barrier
; #define LAS __attribute__((address_space(3)))
; __device__ __forceinline__ unsigned cvt_pk_bf16(float lo, float hi) { const float __attribute__((ext_vector_type(2))) v = {lo, hi}; return __builtin_bit_cast(unsigned, __builtin_convertvector(v, bf16x2_t)); }
; template <bool LOCAL>
; __device__ __forceinline__ void na_unit(const bf16* P, const bf16* VT, bf16* YCAT, const LAS float* rpb_l, LAS bf16* buf, int b, int gr, int hp, int qblk, int tid) {
;     ...
;             const int c = sidx - NCH;
;             if (LOCAL && c < 8) {
;                 float p[8];
; #pragma unroll
;                 for (int e = 0; e < 4; ++e) { p[e] = __expf(sl[2 * (c < 8 ? c : 0)][e] - m); p[4 + e] = __expf(sl[2 * (c < 8 ? c : 0) + 1][e] - m); }
; #pragma unroll
;                 for (int e = 0; e < 8; ++e) lsum += p[e];
;                 const bf16x8 pf = __builtin_bit_cast(bf16x8, (v4u){pg8::cvt_pk_bf16(p[0], p[1]), pg8::cvt_pk_bf16(p[2], p[3]), pg8::cvt_pk_bf16(p[4], p[5]), pg8::cvt_pk_bf16(p[6], p[7])});
; #pragma unroll
;                 for (int dt = 0; dt < 4; ++dt) { const LAS bf16* vp = cb + (16 * dt + fr) * 72 + kc0 + 4 * fq;
;                     o[dt] = __builtin_amdgcn_mfma_f32_16x16x32_bf16(frag44(vp, vp + 16), pf, o[dt], 0, 0, 0); }
;             } else {
;                 const int cc = c - NLOC;
; #pragma unroll
;                 for (int p2 = 0; p2 < 2; ++p2) {
;                     float p[8];
; #pragma unroll
;                     for (int e = 0; e < 4; ++e) { p[e] = __expf(sc[4 * (cc >= 0 ? cc : 0) + 2 * p2][e] - m); p[4 + e] = __expf(sc[4 * (cc >= 0 ? cc : 0) + 2 * p2 + 1][e] - m); }
; #pragma unroll
;                     for (int e = 0; e < 8; ++e) lsum += p[e];
;                     const bf16x8 pf = __builtin_bit_cast(bf16x8, (v4u){pg8::cvt_pk_bf16(p[0], p[1]), pg8::cvt_pk_bf16(p[2], p[3]), pg8::cvt_pk_bf16(p[4], p[5]), pg8::cvt_pk_bf16(p[6], p[7])});
; #pragma unroll
;                     for (int dt = 0; dt < 4; ++dt) { const LAS bf16* vp = cb + (16 * dt + fr) * 72 + 32 * p2 + 4 * fq;
;                         o[dt] = __builtin_amdgcn_mfma_f32_16x16x32_bf16(frag44(vp, vp + 16), pf, o[dt], 0, 0, 0); }
;                 }
;             }
;         }
;         if (sidx + 1 < 2 * NCH) NA_STORE(sidx + 1);
	v_exp_f32_e32 v123, v9
	v_sub_f32_e32 v9, v126, v137
	ds_read2_b64 v[188:191], v8 offset1:4
	ds_read2_b64 v[192:195], v7 offset0:32 offset1:36
	v_mul_f32_e32 v9, 0x3fb8aa3b, v9
	v_exp_f32_e32 v125, v9
	v_sub_f32_e32 v9, v129, v137
	v_mul_f32_e32 v9, 0x3fb8aa3b, v9
	v_exp_f32_e32 v126, v9
	v_lshl_add_u64 v[168:169], s[22:23], 1, v[78:79]
	v_cvt_pk_bf16_f32 v196, v120, v122
	v_cvt_pk_bf16_f32 v197, v124, v125
	v_cvt_pk_bf16_f32 v198, v119, v121
	v_cvt_pk_bf16_f32 v199, v123, v126
	v_lshl_add_u64 v[128:129], v[168:169], 0, v[70:71]
	v_lshl_add_u64 v[168:169], v[168:169], 0, v[80:81]
	s_waitcnt lgkmcnt(1)
	v_mfma_f32_16x16x32_bf16 v[164:167], v[188:191], v[196:199], v[164:167]
	ds_read2_b64 v[188:191], v6 offset0:64 offset1:68
	v_sub_f32_e32 v9, v132, v137
	v_mul_f32_e32 v9, 0x3fb8aa3b, v9
	s_waitcnt lgkmcnt(1)
	v_mfma_f32_16x16x32_bf16 v[176:179], v[192:195], v[196:199], v[176:179]
	v_lshl_add_u64 v[248:249], v[128:129], 0, 0
	v_lshl_add_u64 v[238:239], v[168:169], 0, 0
	global_load_dwordx4 v[192:195], v[128:129], off
	global_load_dwordx4 v[200:203], v[168:169], off
	global_load_dword v250, v[248:249], off offset:128
	global_load_dword v251, v[238:239], off offset:128
	v_exp_f32_e32 v128, v9
	v_sub_f32_e32 v9, v140, v137
	v_mul_f32_e32 v9, 0x3fb8aa3b, v9
	v_exp_f32_e32 v127, v9
	v_sub_f32_e32 v9, v131, v137
	v_mul_f32_e32 v9, 0x3fb8aa3b, v9
	v_exp_f32_e32 v130, v9
	v_sub_f32_e32 v9, v138, v137
	v_mul_f32_e32 v9, 0x3fb8aa3b, v9
	v_exp_f32_e32 v129, v9
	v_sub_f32_e32 v9, v136, v137
	v_mul_f32_e32 v9, 0x3fb8aa3b, v9
	v_exp_f32_e32 v132, v9
	v_sub_f32_e32 v9, v143, v137
	s_waitcnt lgkmcnt(0)
	v_mfma_f32_16x16x32_bf16 v[180:183], v[188:191], v[196:199], v[180:183]
	ds_read2_b64 v[188:191], v159 offset0:96 offset1:100
	v_mul_f32_e32 v9, 0x3fb8aa3b, v9
	s_waitcnt vmcnt(7)
	ds_write_b128 v75, v[184:187] offset:18432
	s_waitcnt vmcnt(6)
	ds_write_b128 v75, v[204:207] offset:27648
	s_waitcnt lgkmcnt(0)
	s_barrier
	v_exp_f32_e32 v131, v9
	v_sub_f32_e32 v9, v135, v137
	ds_read2_b64 v[184:187], v161 offset1:4
	v_mul_f32_e32 v9, 0x3fb8aa3b, v9
	v_exp_f32_e32 v134, v9
	v_sub_f32_e32 v9, v139, v137
	v_mul_f32_e32 v9, 0x3fb8aa3b, v9
	v_exp_f32_e32 v135, v9
	v_lshl_add_u64 v[168:169], s[24:25], 1, v[78:79]
	v_mfma_f32_16x16x32_bf16 v[172:175], v[188:191], v[196:199], v[172:175]
	v_lshl_add_u64 v[204:205], v[168:169], 0, v[70:71]
	v_cvt_pk_bf16_f32 v196, v128, v130
	v_cvt_pk_bf16_f32 v197, v132, v134
	v_cvt_pk_bf16_f32 v198, v127, v129
	v_cvt_pk_bf16_f32 v199, v131, v135
	ds_read2_b64 v[188:191], v160 offset0:32 offset1:36
	v_lshl_add_u64 v[138:139], v[168:169], 0, v[80:81]
	s_waitcnt lgkmcnt(1)
	v_mfma_f32_16x16x32_bf16 v[164:167], v[184:187], v[196:199], v[164:167]
	global_load_dwordx4 v[184:187], v[204:205], off
	s_nop 0
	global_load_dwordx4 v[204:207], v[138:139], off
	v_sub_f32_e32 v9, v142, v137
	v_mul_f32_e32 v9, 0x3fb8aa3b, v9
	s_waitcnt lgkmcnt(0)
	v_mfma_f32_16x16x32_bf16 v[176:179], v[188:191], v[196:199], v[176:179]
	ds_read2_b64 v[188:191], v162 offset0:64 offset1:68
	v_exp_f32_e32 v138, v9
	v_sub_f32_e32 v9, v148, v137
	s_waitcnt lgkmcnt(0)
	v_mfma_f32_16x16x32_bf16 v[180:183], v[188:191], v[196:199], v[180:183]
	ds_read2_b64 v[188:191], v163 offset0:96 offset1:100
	v_mul_f32_e32 v9, 0x3fb8aa3b, v9
	v_exp_f32_e32 v136, v9
	v_sub_f32_e32 v9, v141, v137
	v_mul_f32_e32 v9, 0x3fb8aa3b, v9
	v_exp_f32_e32 v140, v9
	v_sub_f32_e32 v9, v146, v137
	v_mul_f32_e32 v9, 0x3fb8aa3b, v9
	v_exp_f32_e32 v139, v9
	v_sub_f32_e32 v9, v145, v137
	v_mul_f32_e32 v9, 0x3fb8aa3b, v9
	s_waitcnt lgkmcnt(0)
	v_mfma_f32_16x16x32_bf16 v[172:175], v[188:191], v[196:199], v[172:175]
	s_waitcnt vmcnt(5)
	ds_write_b128 v75, v[192:195]
	s_waitcnt vmcnt(4)
	ds_write_b128 v75, v[200:203] offset:9216
	s_waitcnt lgkmcnt(0)
	s_barrier
	v_exp_f32_e32 v142, v9
	v_sub_f32_e32 v9, v151, v137
	ds_read2_b64 v[188:191], v8 offset1:4
	v_mul_f32_e32 v9, 0x3fb8aa3b, v9
	ds_read2_b64 v[196:199], v7 offset0:32 offset1:36
	v_exp_f32_e32 v141, v9
	v_sub_f32_e32 v9, v144, v137
	v_sub_f32_e32 v8, v147, v137
	v_mul_f32_e32 v9, 0x3fb8aa3b, v9
	v_mul_f32_e32 v8, 0x3fb8aa3b, v8
	v_exp_f32_e32 v143, v9
	v_exp_f32_e32 v144, v8
	v_cvt_pk_bf16_f32 v192, v138, v140
	v_cvt_pk_bf16_f32 v194, v136, v139
	v_cvt_pk_bf16_f32 v193, v142, v143
	v_cvt_pk_bf16_f32 v195, v141, v144
	v_lshl_add_u64 v[8:9], s[26:27], 1, v[78:79]
	v_sub_f32_e32 v146, v152, v137
	s_waitcnt lgkmcnt(1)
	v_mfma_f32_16x16x32_bf16 v[164:167], v[188:191], v[192:195], v[164:167]
	ds_read2_b64 v[188:191], v6 offset0:64 offset1:68
	v_lshl_add_u64 v[6:7], v[8:9], 0, v[70:71]
	v_lshl_add_u64 v[8:9], v[8:9], 0, v[80:81]
	s_waitcnt lgkmcnt(1)
	v_mfma_f32_16x16x32_bf16 v[176:179], v[196:199], v[192:195], v[176:179]
	v_lshl_add_u64 v[248:249], v[6:7], 0, 0
	v_lshl_add_u64 v[238:239], v[8:9], 0, 0
	global_load_dwordx4 v[196:199], v[6:7], off
	global_load_dwordx4 v[200:203], v[8:9], off
	global_load_dword v250, v[248:249], off offset:128
	global_load_dword v251, v[238:239], off offset:128
	ds_read2_b64 v[78:81], v159 offset0:96 offset1:100
	s_waitcnt vmcnt(5)
	ds_write_b128 v75, v[184:187] offset:18432
	s_waitcnt vmcnt(4)
	ds_write_b128 v75, v[204:207] offset:27648
	s_waitcnt lgkmcnt(2)
	v_mfma_f32_16x16x32_bf16 v[172:175], v[78:81], v[192:195], v[172:175]
	s_waitcnt lgkmcnt(0)
	s_barrier
; #define LAS __attribute__((address_space(3)))
; __device__ __forceinline__ unsigned cvt_pk_bf16(float lo, float hi) { const float __attribute__((ext_vector_type(2))) v = {lo, hi}; return __builtin_bit_cast(unsigned, __builtin_convertvector(v, bf16x2_t)); }
; #define NA_STORE(sidx) do { LAS bf16* d_ = buf + ((sidx) & 1) * 9216; _Pragma("unroll") for (int q_ = 0; q_ < 2; ++q_) *(LAS v4u*)(d_ + q_ * 4608 + lrow * 72 + lseg * 8) = ld[(sidx) & 1][q_]; } while (0)
; template <bool LOCAL>
; __device__ __forceinline__ void na_unit(const bf16* P, const bf16* VT, bf16* YCAT, const LAS float* rpb_l, LAS bf16* buf, int b, int gr, int hp, int qblk, int tid) {
;     ...
;             } else {
;                 const int cc = c - NLOC;
; #pragma unroll
;                 for (int p2 = 0; p2 < 2; ++p2) {
;                     float p[8];
; #pragma unroll
;                     for (int e = 0; e < 4; ++e) { p[e] = __expf(sc[4 * (cc >= 0 ? cc : 0) + 2 * p2][e] - m); p[4 + e] = __expf(sc[4 * (cc >= 0 ? cc : 0) + 2 * p2 + 1][e] - m); }
; #pragma unroll
;                     for (int e = 0; e < 8; ++e) lsum += p[e];
;                     const bf16x8 pf = __builtin_bit_cast(bf16x8, (v4u){pg8::cvt_pk_bf16(p[0], p[1]), pg8::cvt_pk_bf16(p[2], p[3]), pg8::cvt_pk_bf16(p[4], p[5]), pg8::cvt_pk_bf16(p[6], p[7])});
; #pragma unroll
;                     for (int dt = 0; dt < 4; ++dt) { const LAS bf16* vp = cb + (16 * dt + fr) * 72 + 32 * p2 + 4 * fq;
;                         o[dt] = __builtin_amdgcn_mfma_f32_16x16x32_bf16(frag44(vp, vp + 16), pf, o[dt], 0, 0, 0); }
;                 }
;             }
;         }
;         if (sidx + 1 < 2 * NCH) NA_STORE(sidx + 1);
	v_sub_f32_e32 v70, v150, v137
	v_sub_f32_e32 v79, v149, v137
	v_sub_f32_e32 v81, v153, v137
	ds_read2_b64 v[148:151], v161 offset1:4
	v_mul_f32_e32 v70, 0x3fb8aa3b, v70
	v_mul_f32_e32 v79, 0x3fb8aa3b, v79
	v_mul_f32_e32 v81, 0x3fb8aa3b, v81
	v_mul_f32_e32 v146, 0x3fb8aa3b, v146
	v_exp_f32_e32 v78, v70
	v_sub_f32_e32 v70, v156, v137
	v_exp_f32_e32 v80, v79
	v_sub_f32_e32 v79, v154, v137
	v_exp_f32_e32 v145, v81
	v_sub_f32_e32 v81, v158, v137
	v_exp_f32_e32 v147, v146
	v_sub_f32_e32 v146, v155, v137
	v_mul_f32_e32 v70, 0x3fb8aa3b, v70
	v_mul_f32_e32 v79, 0x3fb8aa3b, v79
	v_mul_f32_e32 v81, 0x3fb8aa3b, v81
	v_mul_f32_e32 v146, 0x3fb8aa3b, v146
	v_exp_f32_e32 v70, v70
	v_exp_f32_e32 v79, v79
	v_exp_f32_e32 v81, v81
	v_exp_f32_e32 v146, v146
	v_cvt_pk_bf16_f32 v152, v78, v80
	v_cvt_pk_bf16_f32 v153, v145, v147
	v_cvt_pk_bf16_f32 v154, v70, v79
	v_cvt_pk_bf16_f32 v155, v81, v146
	v_mfma_f32_16x16x32_bf16 v[180:183], v[188:191], v[192:195], v[180:183]
	v_fma_f32 v62, v62, s74, -v137
	v_fma_f32 v63, v63, s74, -v137
	v_fma_f32 v64, v64, s74, -v137
	s_waitcnt lgkmcnt(0)
	v_mfma_f32_16x16x32_bf16 v[164:167], v[148:151], v[152:155], v[164:167]
	ds_read2_b64 v[148:151], v160 offset0:32 offset1:36
	v_fma_f32 v65, v65, s74, -v137
	v_mul_f32_e32 v62, 0x3fb8aa3b, v62
	s_waitcnt lgkmcnt(0)
	v_mfma_f32_16x16x32_bf16 v[158:161], v[148:151], v[152:155], v[176:179]
	ds_read2_b64 v[148:151], v162 offset0:64 offset1:68
	v_mul_f32_e32 v63, 0x3fb8aa3b, v63
	v_mul_f32_e32 v64, 0x3fb8aa3b, v64
	s_waitcnt lgkmcnt(0)
	v_mfma_f32_16x16x32_bf16 v[176:179], v[148:151], v[152:155], v[180:183]
	ds_read2_b64 v[148:151], v163 offset0:96 offset1:100
	s_nop 1
	v_lshl_add_u64 v[248:249], v[6:7], 0, 0
	v_lshl_add_u64 v[238:239], v[8:9], 0, 0
	global_load_dwordx4 v[180:183], v[6:7], off offset:128
	global_load_dwordx4 v[184:187], v[8:9], off offset:128
	global_load_dword v250, v[248:249], off offset:256
	global_load_dword v251, v[238:239], off offset:256
	s_waitcnt vmcnt(7)
	ds_write_b128 v75, v[196:199]
	s_waitcnt vmcnt(6)
	ds_write_b128 v75, v[200:203] offset:9216
	s_waitcnt lgkmcnt(2)
	v_mfma_f32_16x16x32_bf16 v[150:153], v[148:151], v[152:155], v[172:175]
	s_waitcnt lgkmcnt(0)
	s_barrier
	s_nop 0
	ds_read2_b64 v[172:175], v157 offset1:4
	v_mul_f32_e32 v65, 0x3fb8aa3b, v65
	v_exp_f32_e32 v148, v62
	v_fma_f32 v62, v66, s74, -v137
	v_exp_f32_e32 v66, v63
	v_fma_f32 v63, v67, s74, -v137
	v_exp_f32_e32 v67, v64
	v_fma_f32 v64, v68, s74, -v137
	v_exp_f32_e32 v68, v65
	v_fma_f32 v65, v69, s74, -v137
	v_mul_f32_e32 v62, 0x3fb8aa3b, v62
	v_mul_f32_e32 v63, 0x3fb8aa3b, v63
	v_mul_f32_e32 v64, 0x3fb8aa3b, v64
	v_mul_f32_e32 v65, 0x3fb8aa3b, v65
	v_exp_f32_e32 v62, v62
	v_exp_f32_e32 v63, v63
	v_exp_f32_e32 v64, v64
	v_exp_f32_e32 v65, v65
	v_cvt_pk_bf16_f32 v188, v148, v66
	v_cvt_pk_bf16_f32 v189, v67, v68
	v_cvt_pk_bf16_f32 v190, v62, v63
	v_cvt_pk_bf16_f32 v191, v64, v65
	v_add_u32_e32 v149, 0x800, v157
	v_add_u32_e32 v155, 0x1800, v157
	s_waitcnt lgkmcnt(0)
	v_mfma_f32_16x16x32_bf16 v[162:165], v[172:175], v[188:191], v[164:167]
	ds_read2_b64 v[172:175], v155 offset0:96 offset1:100
	v_add_u32_e32 v154, 0x1000, v157
	v_fma_f32 v58, v58, s74, -v137
	ds_read2_b64 v[166:169], v149 offset0:32 offset1:36
	s_waitcnt lgkmcnt(0)
	v_mfma_f32_16x16x32_bf16 v[158:161], v[166:169], v[188:191], v[158:161]
	ds_read2_b64 v[166:169], v154 offset0:64 offset1:68
	v_fma_f32 v54, v54, s74, -v137
	v_fma_f32 v59, v59, s74, -v137
	v_mfma_f32_16x16x32_bf16 v[150:153], v[172:175], v[188:191], v[150:153]
	ds_read2_b64 v[172:175], v157 offset0:8 offset1:12
	v_fma_f32 v55, v55, s74, -v137
	v_fma_f32 v60, v60, s74, -v137
	v_fma_f32 v56, v56, s74, -v137
	v_fma_f32 v61, v61, s74, -v137
	v_fma_f32 v57, v57, s74, -v137
	v_mul_f32_e32 v58, 0x3fb8aa3b, v58
	v_mul_f32_e32 v54, 0x3fb8aa3b, v54
	v_mul_f32_e32 v59, 0x3fb8aa3b, v59
	v_mul_f32_e32 v55, 0x3fb8aa3b, v55
	v_mul_f32_e32 v60, 0x3fb8aa3b, v60
	v_mul_f32_e32 v56, 0x3fb8aa3b, v56
	v_mul_f32_e32 v61, 0x3fb8aa3b, v61
	v_mul_f32_e32 v57, 0x3fb8aa3b, v57
	v_exp_f32_e32 v58, v58
	v_exp_f32_e32 v54, v54
	v_exp_f32_e32 v59, v59
	v_exp_f32_e32 v55, v55
	v_exp_f32_e32 v60, v60
	v_exp_f32_e32 v56, v56
	v_exp_f32_e32 v61, v61
	v_exp_f32_e32 v57, v57
	s_waitcnt lgkmcnt(1)
	v_mfma_f32_16x16x32_bf16 v[166:169], v[166:169], v[188:191], v[176:179]
	v_fma_f32 v46, v46, s74, -v137
	v_fma_f32 v47, v47, s74, -v137
	v_fma_f32 v48, v48, s74, -v137
	v_cvt_pk_bf16_f32 v176, v58, v59
	v_cvt_pk_bf16_f32 v177, v60, v61
	v_cvt_pk_bf16_f32 v178, v54, v55
	v_cvt_pk_bf16_f32 v179, v56, v57
	v_mul_f32_e32 v46, 0x3fb8aa3b, v46
	v_mul_f32_e32 v47, 0x3fb8aa3b, v47
	s_waitcnt lgkmcnt(0)
	v_mfma_f32_16x16x32_bf16 v[162:165], v[172:175], v[176:179], v[162:165]
	ds_read2_b64 v[172:175], v149 offset0:40 offset1:44
	v_mul_f32_e32 v48, 0x3fb8aa3b, v48
	v_exp_f32_e32 v69, v46
	s_waitcnt lgkmcnt(0)
	v_mfma_f32_16x16x32_bf16 v[158:161], v[172:175], v[176:179], v[158:161]
	ds_read2_b64 v[172:175], v154 offset0:72 offset1:76
	v_fma_f32 v46, v50, s74, -v137
	v_exp_f32_e32 v50, v47
	s_waitcnt lgkmcnt(0)
	v_mfma_f32_16x16x32_bf16 v[166:169], v[172:175], v[176:179], v[166:169]
	ds_read2_b64 v[172:175], v155 offset0:104 offset1:108
	v_fma_f32 v47, v51, s74, -v137
	v_exp_f32_e32 v51, v48
	v_fma_f32 v48, v52, s74, -v137
	v_add_u32_e32 v52, 0x4800, v157
	v_lshl_add_u64 v[248:249], v[6:7], 0, 0
	v_lshl_add_u64 v[238:239], v[8:9], 0, 0
	global_load_dwordx4 v[188:191], v[6:7], off offset:256
	global_load_dwordx4 v[192:195], v[8:9], off offset:256
	global_load_dword v250, v[248:249], off offset:384
	global_load_dword v251, v[238:239], off offset:384
	s_waitcnt lgkmcnt(0)
	v_mfma_f32_16x16x32_bf16 v[150:153], v[172:175], v[176:179], v[150:153]
	s_waitcnt vmcnt(7)
	ds_write_b128 v75, v[180:183] offset:18432
	s_waitcnt vmcnt(6)
	ds_write_b128 v75, v[184:187] offset:27648
	s_waitcnt lgkmcnt(0)
	s_barrier
; #define LAS __attribute__((address_space(3)))
; __device__ __forceinline__ unsigned cvt_pk_bf16(float lo, float hi) { const float __attribute__((ext_vector_type(2))) v = {lo, hi}; return __builtin_bit_cast(unsigned, __builtin_convertvector(v, bf16x2_t)); }
; #define NA_STORE(sidx) do { LAS bf16* d_ = buf + ((sidx) & 1) * 9216; _Pragma("unroll") for (int q_ = 0; q_ < 2; ++q_) *(LAS v4u*)(d_ + q_ * 4608 + lrow * 72 + lseg * 8) = ld[(sidx) & 1][q_]; } while (0)
; template <bool LOCAL>
; __device__ __forceinline__ void na_unit(const bf16* P, const bf16* VT, bf16* YCAT, const LAS float* rpb_l, LAS bf16* buf, int b, int gr, int hp, int qblk, int tid) {
;     ...
;             } else {
;                 const int cc = c - NLOC;
; #pragma unroll
;                 for (int p2 = 0; p2 < 2; ++p2) {
;                     float p[8];
; #pragma unroll
;                     for (int e = 0; e < 4; ++e) { p[e] = __expf(sc[4 * (cc >= 0 ? cc : 0) + 2 * p2][e] - m); p[4 + e] = __expf(sc[4 * (cc >= 0 ? cc : 0) + 2 * p2 + 1][e] - m); }
; #pragma unroll
;                     for (int e = 0; e < 8; ++e) lsum += p[e];
;                     const bf16x8 pf = __builtin_bit_cast(bf16x8, (v4u){pg8::cvt_pk_bf16(p[0], p[1]), pg8::cvt_pk_bf16(p[2], p[3]), pg8::cvt_pk_bf16(p[4], p[5]), pg8::cvt_pk_bf16(p[6], p[7])});
; #pragma unroll
;                     for (int dt = 0; dt < 4; ++dt) { const LAS bf16* vp = cb + (16 * dt + fr) * 72 + 32 * p2 + 4 * fq;
;                         o[dt] = __builtin_amdgcn_mfma_f32_16x16x32_bf16(frag44(vp, vp + 16), pf, o[dt], 0, 0, 0); }
;                 }
;             }
;         }
;         if (sidx + 1 < 2 * NCH) NA_STORE(sidx + 1);
	v_fma_f32 v49, v49, s74, -v137
	ds_read2_b64 v[172:175], v52 offset1:4
	v_mul_f32_e32 v49, 0x3fb8aa3b, v49
	v_exp_f32_e32 v156, v49
	v_fma_f32 v49, v53, s74, -v137
	v_mul_f32_e32 v46, 0x3fb8aa3b, v46
	v_mul_f32_e32 v47, 0x3fb8aa3b, v47
	v_mul_f32_e32 v48, 0x3fb8aa3b, v48
	v_mul_f32_e32 v49, 0x3fb8aa3b, v49
	v_exp_f32_e32 v46, v46
	v_exp_f32_e32 v47, v47
	v_exp_f32_e32 v48, v48
	v_exp_f32_e32 v53, v49
	v_cvt_pk_bf16_f32 v176, v69, v50
	v_cvt_pk_bf16_f32 v177, v51, v156
	v_cvt_pk_bf16_f32 v178, v46, v47
	v_cvt_pk_bf16_f32 v179, v48, v53
	v_add_u32_e32 v180, 0x5000, v157
	v_add_u32_e32 v181, 0x5800, v157
	s_waitcnt lgkmcnt(0)
	v_mfma_f32_16x16x32_bf16 v[162:165], v[172:175], v[176:179], v[162:165]
	ds_read2_b64 v[172:175], v180 offset0:32 offset1:36
	v_add_u32_e32 v49, 0x6000, v157
	v_fma_f32 v38, v38, s74, -v137
	s_waitcnt lgkmcnt(0)
	v_mfma_f32_16x16x32_bf16 v[158:161], v[172:175], v[176:179], v[158:161]
	ds_read2_b64 v[172:175], v181 offset0:64 offset1:68
	v_mul_f32_e32 v38, 0x3fb8aa3b, v38
	v_fma_f32 v42, v42, s74, -v137
	s_waitcnt lgkmcnt(0)
	v_mfma_f32_16x16x32_bf16 v[166:169], v[172:175], v[176:179], v[166:169]
	ds_read2_b64 v[172:175], v49 offset0:96 offset1:100
	v_mul_f32_e32 v42, 0x3fb8aa3b, v42
	v_fma_f32 v30, v30, s74, -v137
	s_waitcnt lgkmcnt(0)
	v_mfma_f32_16x16x32_bf16 v[150:153], v[172:175], v[176:179], v[150:153]
	v_exp_f32_e32 v177, v38
	v_fma_f32 v38, v43, s74, -v137
	v_mul_f32_e32 v38, 0x3fb8aa3b, v38
	v_exp_f32_e32 v178, v38
	v_fma_f32 v38, v39, s74, -v137
	v_mul_f32_e32 v38, 0x3fb8aa3b, v38
	v_exp_f32_e32 v179, v38
	v_fma_f32 v38, v44, s74, -v137
	v_mul_f32_e32 v38, 0x3fb8aa3b, v38
	v_exp_f32_e32 v182, v38
	v_fma_f32 v38, v40, s74, -v137
	v_mul_f32_e32 v38, 0x3fb8aa3b, v38
	v_exp_f32_e32 v176, v42
	v_exp_f32_e32 v183, v38
	v_fma_f32 v38, v45, s74, -v137
	ds_read2_b64 v[42:45], v52 offset0:8 offset1:12
	v_mul_f32_e32 v38, 0x3fb8aa3b, v38
	v_exp_f32_e32 v184, v38
	v_fma_f32 v38, v41, s74, -v137
	v_mul_f32_e32 v38, 0x3fb8aa3b, v38
	v_exp_f32_e32 v185, v38
	v_cvt_pk_bf16_f32 v38, v176, v178
	v_cvt_pk_bf16_f32 v39, v182, v184
	v_cvt_pk_bf16_f32 v40, v177, v179
	v_cvt_pk_bf16_f32 v41, v183, v185
	v_mul_f32_e32 v30, 0x3fb8aa3b, v30
	v_fma_f32 v22, v22, s74, -v137
	s_waitcnt lgkmcnt(0)
	v_mfma_f32_16x16x32_bf16 v[42:45], v[42:45], v[38:41], v[162:165]
	v_mul_f32_e32 v22, 0x3fb8aa3b, v22
	v_fma_f32 v26, v26, s74, -v137
	v_mul_f32_e32 v26, 0x3fb8aa3b, v26
	ds_read2_b64 v[162:165], v180 offset0:40 offset1:44
	s_waitcnt lgkmcnt(0)
	v_mfma_f32_16x16x32_bf16 v[158:161], v[162:165], v[38:41], v[158:161]
	ds_read2_b64 v[162:165], v181 offset0:72 offset1:76
	v_fma_f32 v2, v2, s74, -v137
	v_mul_f32_e32 v2, 0x3fb8aa3b, v2
	s_waitcnt lgkmcnt(0)
	v_mfma_f32_16x16x32_bf16 v[162:165], v[162:165], v[38:41], v[166:169]
	s_nop 2
	ds_read2_b64 v[166:169], v49 offset0:104 offset1:108
	global_load_dwordx4 v[172:175], v[6:7], off offset:384
	s_nop 0
	global_load_dwordx4 v[6:9], v[8:9], off offset:384
	s_waitcnt vmcnt(5)
	ds_write_b128 v75, v[188:191]
	s_waitcnt vmcnt(4)
	ds_write_b128 v75, v[192:195] offset:9216
	s_waitcnt lgkmcnt(2)
	v_mfma_f32_16x16x32_bf16 v[38:41], v[166:169], v[38:41], v[150:153]
	v_exp_f32_e32 v166, v30
	v_fma_f32 v30, v34, s74, -v137
	v_mul_f32_e32 v30, 0x3fb8aa3b, v30
	v_exp_f32_e32 v167, v30
	v_fma_f32 v30, v31, s74, -v137
	v_mul_f32_e32 v30, 0x3fb8aa3b, v30
	v_exp_f32_e32 v168, v30
	v_fma_f32 v30, v35, s74, -v137
	v_mul_f32_e32 v30, 0x3fb8aa3b, v30
	v_exp_f32_e32 v169, v30
	v_fma_f32 v30, v32, s74, -v137
	v_mul_f32_e32 v30, 0x3fb8aa3b, v30
	v_exp_f32_e32 v186, v30
	v_fma_f32 v30, v36, s74, -v137
	v_mul_f32_e32 v30, 0x3fb8aa3b, v30
	v_exp_f32_e32 v187, v30
	v_fma_f32 v30, v33, s74, -v137
	s_waitcnt lgkmcnt(0)
	s_barrier
	v_mul_f32_e32 v34, 0x3fb8aa3b, v30
	ds_read2_b64 v[30:33], v157 offset1:4
	v_exp_f32_e32 v188, v34
	v_fma_f32 v34, v37, s74, -v137
	v_mul_f32_e32 v34, 0x3fb8aa3b, v34
	v_exp_f32_e32 v189, v34
	v_cvt_pk_bf16_f32 v34, v166, v168
	v_cvt_pk_bf16_f32 v35, v186, v188
	v_cvt_pk_bf16_f32 v36, v167, v169
	v_cvt_pk_bf16_f32 v37, v187, v189
	ds_read2_b64 v[150:153], v154 offset0:64 offset1:68
	v_fma_f32 v10, v10, s74, -v137
	s_waitcnt lgkmcnt(1)
	v_mfma_f32_16x16x32_bf16 v[30:33], v[30:33], v[34:37], v[42:45]
	v_mul_f32_e32 v10, 0x3fb8aa3b, v10
	s_nop 1
	ds_read2_b64 v[42:45], v149 offset0:32 offset1:36
	s_waitcnt lgkmcnt(0)
	v_mfma_f32_16x16x32_bf16 v[42:45], v[42:45], v[34:37], v[158:161]
	s_nop 2
	ds_read2_b64 v[158:161], v155 offset0:96 offset1:100
	v_mfma_f32_16x16x32_bf16 v[150:153], v[150:153], v[34:37], v[162:165]
	s_waitcnt lgkmcnt(0)
	v_mfma_f32_16x16x32_bf16 v[34:37], v[158:161], v[34:37], v[38:41]
	v_exp_f32_e32 v159, v22
	v_fma_f32 v22, v27, s74, -v137
	v_mul_f32_e32 v22, 0x3fb8aa3b, v22
	v_exp_f32_e32 v160, v22
	v_fma_f32 v22, v23, s74, -v137
	v_mul_f32_e32 v22, 0x3fb8aa3b, v22
	v_exp_f32_e32 v161, v22
	v_fma_f32 v22, v28, s74, -v137
	v_mul_f32_e32 v22, 0x3fb8aa3b, v22
	v_exp_f32_e32 v162, v22
	v_fma_f32 v22, v24, s74, -v137
	v_mul_f32_e32 v22, 0x3fb8aa3b, v22
	v_exp_f32_e32 v158, v26
	v_exp_f32_e32 v163, v22
	v_fma_f32 v22, v29, s74, -v137
	ds_read2_b64 v[26:29], v157 offset0:8 offset1:12
	v_mul_f32_e32 v22, 0x3fb8aa3b, v22
	v_exp_f32_e32 v157, v22
	v_fma_f32 v22, v25, s74, -v137
	v_mul_f32_e32 v22, 0x3fb8aa3b, v22
	v_exp_f32_e32 v164, v22
	v_cvt_pk_bf16_f32 v22, v158, v160
	v_cvt_pk_bf16_f32 v23, v162, v157
	v_cvt_pk_bf16_f32 v24, v159, v161
	v_cvt_pk_bf16_f32 v25, v163, v164
	ds_read2_b64 v[38:41], v154 offset0:72 offset1:76
	s_waitcnt lgkmcnt(1)
	v_mfma_f32_16x16x32_bf16 v[26:29], v[26:29], v[22:25], v[30:33]
	s_nop 2
	ds_read2_b64 v[30:33], v149 offset0:40 offset1:44
	s_waitcnt lgkmcnt(0)
	v_mfma_f32_16x16x32_bf16 v[30:33], v[30:33], v[22:25], v[42:45]
	s_nop 2
	ds_read2_b64 v[42:45], v155 offset0:104 offset1:108
	s_waitcnt vmcnt(1)
	ds_write_b128 v75, v[172:175] offset:18432
	s_waitcnt vmcnt(0)
	ds_write_b128 v75, v[6:9] offset:27648
	v_fma_f32 v6, v14, s74, -v137
	v_mul_f32_e32 v6, 0x3fb8aa3b, v6
	v_mfma_f32_16x16x32_bf16 v[38:41], v[38:41], v[22:25], v[150:153]
	s_waitcnt lgkmcnt(0)
	s_barrier
; #define LAS __attribute__((address_space(3)))
; __device__ __forceinline__ unsigned cvt_pk_bf16(float lo, float hi) { const float __attribute__((ext_vector_type(2))) v = {lo, hi}; return __builtin_bit_cast(unsigned, __builtin_convertvector(v, bf16x2_t)); }
; #define NA_STORE(sidx) do { LAS bf16* d_ = buf + ((sidx) & 1) * 9216; _Pragma("unroll") for (int q_ = 0; q_ < 2; ++q_) *(LAS v4u*)(d_ + q_ * 4608 + lrow * 72 + lseg * 8) = ld[(sidx) & 1][q_]; } while (0)
; template <bool LOCAL>
; __device__ __forceinline__ void na_unit(const bf16* P, const bf16* VT, bf16* YCAT, const LAS float* rpb_l, LAS bf16* buf, int b, int gr, int hp, int qblk, int tid) {
;     ...
;             } else {
;                 const int cc = c - NLOC;
; #pragma unroll
;                 for (int p2 = 0; p2 < 2; ++p2) {
;                     float p[8];
; #pragma unroll
;                     for (int e = 0; e < 4; ++e) { p[e] = __expf(sc[4 * (cc >= 0 ? cc : 0) + 2 * p2][e] - m); p[4 + e] = __expf(sc[4 * (cc >= 0 ? cc : 0) + 2 * p2 + 1][e] - m); }
; #pragma unroll
;                     for (int e = 0; e < 8; ++e) lsum += p[e];
;                     const bf16x8 pf = __builtin_bit_cast(bf16x8, (v4u){pg8::cvt_pk_bf16(p[0], p[1]), pg8::cvt_pk_bf16(p[2], p[3]), pg8::cvt_pk_bf16(p[4], p[5]), pg8::cvt_pk_bf16(p[6], p[7])});
; #pragma unroll
;                     for (int dt = 0; dt < 4; ++dt) { const LAS bf16* vp = cb + (16 * dt + fr) * 72 + 32 * p2 + 4 * fq;
;                         o[dt] = __builtin_amdgcn_mfma_f32_16x16x32_bf16(frag44(vp, vp + 16), pf, o[dt], 0, 0, 0); }
;                 }
;             }
;         }
;         if (sidx + 1 < 2 * NCH) NA_STORE(sidx + 1);
;         __syncthreads();
;     }
;     ...
;     lsum += __shfl_xor(lsum, 16); lsum += __shfl_xor(lsum, 32);
	v_mfma_f32_16x16x32_bf16 v[22:25], v[42:45], v[22:25], v[34:37]
	v_ashrrev_i32_e32 v75, 31, v74
	s_nop 1
	v_exp_f32_e32 v34, v6
	v_fma_f32 v6, v18, s74, -v137
	v_mul_f32_e32 v6, 0x3fb8aa3b, v6
	v_exp_f32_e32 v35, v6
	v_fma_f32 v6, v15, s74, -v137
	v_mul_f32_e32 v6, 0x3fb8aa3b, v6
	v_exp_f32_e32 v36, v6
	v_fma_f32 v6, v19, s74, -v137
	v_mul_f32_e32 v6, 0x3fb8aa3b, v6
	v_exp_f32_e32 v37, v6
	v_fma_f32 v6, v16, s74, -v137
	v_mul_f32_e32 v6, 0x3fb8aa3b, v6
	v_exp_f32_e32 v42, v6
	v_fma_f32 v6, v20, s74, -v137
	v_mul_f32_e32 v6, 0x3fb8aa3b, v6
	v_exp_f32_e32 v43, v6
	v_fma_f32 v6, v17, s74, -v137
	v_mul_f32_e32 v14, 0x3fb8aa3b, v6
	ds_read2_b64 v[6:9], v52 offset1:4
	v_exp_f32_e32 v44, v14
	v_fma_f32 v14, v21, s74, -v137
	v_mul_f32_e32 v14, 0x3fb8aa3b, v14
	v_exp_f32_e32 v45, v14
	v_cvt_pk_bf16_f32 v14, v34, v36
	v_cvt_pk_bf16_f32 v15, v42, v44
	v_cvt_pk_bf16_f32 v16, v35, v37
	v_cvt_pk_bf16_f32 v17, v43, v45
	ds_read2_b64 v[18:21], v180 offset0:32 offset1:36
	s_waitcnt lgkmcnt(1)
	v_mfma_f32_16x16x32_bf16 v[6:9], v[6:9], v[14:17], v[26:29]
	s_nop 2
	ds_read2_b64 v[26:29], v181 offset0:64 offset1:68
	s_waitcnt lgkmcnt(0)
	v_mfma_f32_16x16x32_bf16 v[26:29], v[26:29], v[14:17], v[38:41]
	s_nop 2
	v_add_f32_e32 v38, 0, v133
	v_add_f32_e32 v38, v97, v38
	v_add_f32_e32 v38, v96, v38
	v_add_f32_e32 v38, v100, v38
	v_add_f32_e32 v38, v93, v38
	v_add_f32_e32 v38, v92, v38
	v_add_f32_e32 v38, v95, v38
	v_add_f32_e32 v38, v94, v38
	v_add_f32_e32 v38, v87, v38
	v_add_f32_e32 v38, v91, v38
	v_add_f32_e32 v38, v99, v38
	v_add_f32_e32 v38, v101, v38
	v_add_f32_e32 v38, v76, v38
	v_add_f32_e32 v38, v88, v38
	v_add_f32_e32 v38, v98, v38
	v_add_f32_e32 v38, v102, v38
	v_add_f32_e32 v38, v104, v38
	v_add_f32_e32 v38, v106, v38
	v_add_f32_e32 v38, v108, v38
	v_add_f32_e32 v38, v109, v38
	v_add_f32_e32 v38, v103, v38
	v_add_f32_e32 v38, v105, v38
	v_add_f32_e32 v38, v107, v38
	v_add_f32_e32 v38, v110, v38
	v_add_f32_e32 v38, v112, v38
	v_add_f32_e32 v38, v114, v38
	v_add_f32_e32 v38, v116, v38
	v_add_f32_e32 v38, v117, v38
	v_add_f32_e32 v38, v111, v38
	v_add_f32_e32 v38, v113, v38
	v_add_f32_e32 v38, v115, v38
	v_add_f32_e32 v38, v118, v38
	v_add_f32_e32 v38, v120, v38
	v_add_f32_e32 v38, v122, v38
	v_add_f32_e32 v38, v124, v38
	v_add_f32_e32 v38, v125, v38
	v_add_f32_e32 v38, v119, v38
	v_add_f32_e32 v38, v121, v38
	v_add_f32_e32 v38, v123, v38
	v_add_f32_e32 v38, v126, v38
	v_add_f32_e32 v38, v128, v38
	v_add_f32_e32 v38, v130, v38
	v_add_f32_e32 v38, v132, v38
	v_add_f32_e32 v38, v134, v38
	v_add_f32_e32 v38, v127, v38
	v_add_f32_e32 v38, v129, v38
	v_add_f32_e32 v38, v131, v38
	v_add_f32_e32 v38, v135, v38
	v_add_f32_e32 v38, v138, v38
	v_add_f32_e32 v38, v140, v38
	v_add_f32_e32 v38, v142, v38
	v_add_f32_e32 v38, v143, v38
	v_add_f32_e32 v38, v136, v38
	v_add_f32_e32 v38, v139, v38
	v_add_f32_e32 v38, v141, v38
	v_add_f32_e32 v38, v144, v38
	v_add_f32_e32 v38, v78, v38
	v_add_f32_e32 v38, v80, v38
	v_add_f32_e32 v38, v145, v38
	v_add_f32_e32 v38, v147, v38
	v_add_f32_e32 v38, v70, v38
	v_add_f32_e32 v38, v79, v38
	v_add_f32_e32 v38, v81, v38
	v_add_f32_e32 v38, v146, v38
	v_add_f32_e32 v38, v148, v38
	v_add_f32_e32 v38, v66, v38
	v_add_f32_e32 v38, v67, v38
	v_add_f32_e32 v38, v68, v38
	v_add_f32_e32 v38, v62, v38
	v_add_f32_e32 v38, v63, v38
	v_add_f32_e32 v38, v64, v38
	v_add_f32_e32 v38, v65, v38
	v_add_f32_e32 v38, v58, v38
	v_add_f32_e32 v38, v59, v38
	v_add_f32_e32 v38, v60, v38
	v_add_f32_e32 v38, v61, v38
	v_add_f32_e32 v38, v54, v38
	v_add_f32_e32 v38, v55, v38
	v_add_f32_e32 v38, v56, v38
	v_add_f32_e32 v38, v57, v38
	v_add_f32_e32 v38, v69, v38
	v_add_f32_e32 v38, v50, v38
	v_add_f32_e32 v38, v51, v38
	v_add_f32_e32 v38, v156, v38
	v_add_f32_e32 v38, v46, v38
	v_add_f32_e32 v38, v47, v38
	v_add_f32_e32 v38, v48, v38
	v_add_f32_e32 v38, v53, v38
	v_add_f32_e32 v38, v176, v38
	v_mfma_f32_16x16x32_bf16 v[18:21], v[18:21], v[14:17], v[30:33]
	v_add_f32_e32 v38, v178, v38
	v_add_f32_e32 v38, v182, v38
	v_add_f32_e32 v38, v184, v38
	ds_read2_b64 v[30:33], v49 offset0:96 offset1:100
	v_add_f32_e32 v38, v177, v38
	v_add_f32_e32 v38, v179, v38
	v_add_f32_e32 v38, v183, v38
	v_add_f32_e32 v38, v185, v38
	v_add_f32_e32 v38, v166, v38
	v_add_f32_e32 v38, v168, v38
	s_waitcnt lgkmcnt(0)
	v_mfma_f32_16x16x32_bf16 v[14:17], v[30:33], v[14:17], v[22:25]
	v_add_f32_e32 v38, v186, v38
	s_nop 1
	v_exp_f32_e32 v23, v2
	v_fma_f32 v2, v11, s74, -v137
	v_mul_f32_e32 v2, 0x3fb8aa3b, v2
	v_add_f32_e32 v38, v188, v38
	v_exp_f32_e32 v24, v2
	v_fma_f32 v2, v3, s74, -v137
	v_add_f32_e32 v38, v167, v38
	v_mul_f32_e32 v2, 0x3fb8aa3b, v2
	v_add_f32_e32 v38, v169, v38
	v_exp_f32_e32 v25, v2
	v_fma_f32 v2, v12, s74, -v137
	v_add_f32_e32 v38, v187, v38
	v_mul_f32_e32 v2, 0x3fb8aa3b, v2
	v_add_f32_e32 v38, v189, v38
	v_exp_f32_e32 v30, v2
	v_fma_f32 v2, v4, s74, -v137
	v_add_f32_e32 v38, v158, v38
	v_mul_f32_e32 v2, 0x3fb8aa3b, v2
	v_add_f32_e32 v38, v160, v38
	v_exp_f32_e32 v22, v10
	v_exp_f32_e32 v31, v2
	v_fma_f32 v2, v13, s74, -v137
	ds_read2_b64 v[10:13], v52 offset0:8 offset1:12
	v_add_f32_e32 v38, v162, v38
	v_mul_f32_e32 v2, 0x3fb8aa3b, v2
	v_add_f32_e32 v38, v157, v38
	v_exp_f32_e32 v32, v2
	v_fma_f32 v2, v5, s74, -v137
	v_add_f32_e32 v38, v159, v38
	v_mul_f32_e32 v2, 0x3fb8aa3b, v2
	v_add_f32_e32 v38, v161, v38
	v_exp_f32_e32 v33, v2
	v_add_f32_e32 v38, v163, v38
	v_add_f32_e32 v38, v164, v38
	v_add_f32_e32 v34, v34, v38
	v_add_f32_e32 v34, v36, v34
	v_cvt_pk_bf16_f32 v2, v22, v24
	v_cvt_pk_bf16_f32 v3, v30, v32
	v_cvt_pk_bf16_f32 v4, v23, v25
	v_cvt_pk_bf16_f32 v5, v31, v33
	v_add_f32_e32 v34, v42, v34
	v_add_f32_e32 v34, v44, v34
	s_waitcnt lgkmcnt(0)
	v_mfma_f32_16x16x32_bf16 v[6:9], v[10:13], v[2:5], v[6:9]
	ds_read2_b64 v[10:13], v180 offset0:40 offset1:44
	v_add_f32_e32 v34, v35, v34
	v_add_f32_e32 v34, v37, v34
	v_add_f32_e32 v34, v43, v34
	v_add_f32_e32 v34, v45, v34
	v_add_f32_e32 v22, v22, v34
	v_add_f32_e32 v22, v24, v22
	v_add_f32_e32 v22, v30, v22
	v_add_f32_e32 v22, v32, v22
	s_waitcnt lgkmcnt(0)
	v_mfma_f32_16x16x32_bf16 v[10:13], v[10:13], v[2:5], v[18:21]
	v_add_f32_e32 v22, v23, v22
	v_add_f32_e32 v22, v25, v22
	v_add_f32_e32 v22, v31, v22
	ds_read2_b64 v[18:21], v181 offset0:72 offset1:76
	v_add_f32_e32 v30, v33, v22
	ds_bpermute_b32 v31, v89, v30
	ds_read2_b64 v[22:25], v49 offset0:104 offset1:108
	s_waitcnt lgkmcnt(2)
	v_mfma_f32_16x16x32_bf16 v[18:21], v[18:21], v[2:5], v[26:29]
	s_waitcnt lgkmcnt(1)
	s_nop 1
	v_add_f32_e32 v26, v30, v31
	ds_bpermute_b32 v27, v90, v26
	v_lshlrev_b32_e32 v70, 1, v77
	s_waitcnt lgkmcnt(1)
	v_mfma_f32_16x16x32_bf16 v[14:17], v[22:25], v[2:5], v[14:17]
	s_waitcnt lgkmcnt(0)
	s_barrier
; __device__ __forceinline__ unsigned cvt_pk_bf16(float lo, float hi) { const float __attribute__((ext_vector_type(2))) v = {lo, hi}; return __builtin_bit_cast(unsigned, __builtin_convertvector(v, bf16x2_t)); }
; template <bool LOCAL>
; __device__ __forceinline__ void na_unit(const bf16* P, const bf16* VT, bf16* YCAT, const LAS float* rpb_l, LAS bf16* buf, int b, int gr, int hp, int qblk, int tid) {
;     ...
;     lsum += __shfl_xor(lsum, 16); lsum += __shfl_xor(lsum, 32);
;     const float inv = 1.f / lsum;
;     bf16* op = YCAT + (size_t)(qrow0 + fr) * D + 512 + h * 64 + 4 * fq;
; #pragma unroll
;     for (int dt = 0; dt < 4; ++dt) { v2u w; w.x = pg8::cvt_pk_bf16(o[dt][0] * inv, o[dt][1] * inv); w.y = pg8::cvt_pk_bf16(o[dt][2] * inv, o[dt][3] * inv); *(v2u*)(op + dt * 16) = w; }
	v_add_f32_e32 v2, v26, v27
	v_div_scale_f32 v3, s[0:1], v2, v2, 1.0
	v_rcp_f32_e32 v4, v3
	s_nop 0
	v_fma_f32 v5, -v3, v4, 1.0
	v_fmac_f32_e32 v4, v5, v4
	v_div_scale_f32 v5, vcc, 1.0, v2, 1.0
	v_mul_f32_e32 v22, v5, v4
	v_fma_f32 v23, -v3, v22, v5
	v_fmac_f32_e32 v22, v23, v4
	v_fma_f32 v3, -v3, v22, v5
	v_div_fmas_f32 v3, v3, v4, v22
	v_div_fixup_f32 v22, v3, v2, 1.0
	v_lshlrev_b64 v[2:3], 11, v[74:75]
	v_lshl_add_u64 v[2:3], s[10:11], 0, v[2:3]
	v_lshl_add_u64 v[2:3], v[72:73], 1, v[2:3]
	v_pk_mul_f32 v[6:7], v[6:7], v[22:23] op_sel_hi:[1,0]
	v_pk_mul_f32 v[8:9], v[8:9], v[22:23] op_sel_hi:[1,0]
	v_lshl_add_u64 v[4:5], v[2:3], 0, v[70:71]
	v_cvt_pk_bf16_f32 v6, v6, v7
	v_cvt_pk_bf16_f32 v7, v8, v9
	global_store_dwordx2 v[4:5], v[6:7], off offset:1024
	v_pk_mul_f32 v[6:7], v[10:11], v[22:23] op_sel_hi:[1,0]
	v_pk_mul_f32 v[8:9], v[12:13], v[22:23] op_sel_hi:[1,0]
	v_cvt_pk_bf16_f32 v6, v6, v7
	v_cvt_pk_bf16_f32 v7, v8, v9
	global_store_dwordx2 v[4:5], v[6:7], off offset:1056
	v_pk_mul_f32 v[6:7], v[18:19], v[22:23] op_sel_hi:[1,0]
	v_pk_mul_f32 v[8:9], v[20:21], v[22:23] op_sel_hi:[1,0]
	v_cvt_pk_bf16_f32 v6, v6, v7
	v_cvt_pk_bf16_f32 v7, v8, v9
	v_lshl_add_u64 v[2:3], v[4:5], 0, s[12:13]
	global_store_dwordx2 v[4:5], v[6:7], off offset:1088
	v_pk_mul_f32 v[4:5], v[14:15], v[22:23] op_sel_hi:[1,0]
	v_pk_mul_f32 v[6:7], v[16:17], v[22:23] op_sel_hi:[1,0]
	v_cvt_pk_bf16_f32 v4, v4, v5

; template <bool LOCAL>
; __device__ __forceinline__ void na_unit(const bf16* P, const bf16* VT, bf16* YCAT, const LAS float* rpb_l, LAS bf16* buf, int b, int gr, int hp, int qblk, int tid) {
;     ...
;     const int lane = tid & 63, wv = tid >> 6, fr = lane & 15, fq = lane >> 4, hh = wv >> 2, qb = wv & 3, h = 2 * hp + hh;
;     const int qrow0 = LOCAL ? NCTX + b * SEQ + gr * 64 + 16 * qb : b * CTXL + qblk * 64 + 16 * qb;
;     const int r0 = min(max(gr - 4, 0), 24);
;     const int kc0 = qb == 0 ? 0 : qb == 1 ? 8 : qb == 2 ? 24 : 32;
;     const int qcol = 16 * qb + fr, cs = min(max(qcol - 8, 0), 48);
;     const LAS float* rpb = rpb_l + h * 15 * 31;
;     v4u ld[2][2];
;     const int lrow = (tid >> 3) & 63, lseg = tid & 7;
;     ...
;     bf16x8 qf[2];
; #pragma unroll
;     for (int ks = 0; ks < 2; ++ks) qf[ks] = *(const bf16x8*)(P + (size_t)(qrow0 + fr) * DINP + h * 64 + 32 * ks + 8 * fq);
;     f32x4 sl[16], sc[16];
;     float m = -1.0e30f, lsum = 0.f;
;     f32x4 o[4];
; #pragma unroll
;     for (int dt = 0; dt < 4; ++dt) o[dt] = (f32x4){0.f, 0.f, 0.f, 0.f};
;     NA_ISSUE(0); NA_ISSUE(1); NA_STORE(0);
;     __syncthreads();
; #pragma unroll
;     for (int sidx = 0; sidx < 2 * NCH; ++sidx) {
;         if (sidx + 2 < 2 * NCH) NA_ISSUE(sidx + 2);
;         const LAS bf16* cb = buf + (sidx & 1) * 9216 + hh * 4608;
;         if (sidx < NCH) {
;             const int c = sidx;
;             if (LOCAL && c < 8) {
; #pragma unroll
;                 for (int t2 = 0; t2 < 2; ++t2) {
;                     const LAS bf16* kp = cb + (kc0 + 16 * t2 + fr) * 72 + 8 * fq;
;                     f32x4 acc = {0.f, 0.f, 0.f, 0.f};
;                     acc = __builtin_amdgcn_mfma_f32_16x16x32_bf16(*(const LAS bf16x8*)(kp), qf[0], acc, 0, 0, 0);
;                     acc = __builtin_amdgcn_mfma_f32_16x16x32_bf16(*(const LAS bf16x8*)(kp + 32), qf[1], acc, 0, 0, 0);
;                     const LAS float* rb = rpb + (r0 + c - gr + 7) * 31 + 15 - qcol;
; #pragma unroll
;                     for (int e = 0; e < 4; ++e) { const int kcol = kc0 + 16 * t2 + 4 * fq + e; const bool ok = (kcol >= cs) && (kcol < cs + 16);
;                         const float sv = ok ? acc[e] * 0.125f + rb[ok ? kcol : qcol] : -1.0e30f; acc[e] = sv; m = fmaxf(m, sv); }
;                     sl[2 * (c < 8 ? c : 0) + t2] = acc; }
;             } else {
;                 const int cc = c - NLOC;
; #pragma unroll
.LBB0_2889:
	v_mov_b32_e32 v93, v0
	s_movk_i32 s2, 0x2400
	v_and_b32_e32 v89, 15, v93
	v_bfe_u32 v91, v93, 4, 2
	v_ashrrev_i32_e32 v92, 8, v93
	s_mov_b64 s[0:1], -1
	s_cmpk_gt_i32 s80, 0x7ff
	v_bfe_u32 v88, v93, 3, 6
	v_lshlrev_b32_e32 v76, 3, v91
	v_lshlrev_b32_e32 v70, 4, v91
	v_mad_i32_i24 v86, v92, s2, 0
	v_mul_u32_u24_e32 v87, 0x90, v89
	s_waitcnt lgkmcnt(0)
	s_barrier
	s_cbranch_scc0 .LBB0_2891
	s_lshl_b32 s0, s80, 4
	s_and_b32 s0, s0, 0xffffff00
	s_addk_i32 s0, 0x8000
	v_mov_b64_e32 v[78:79], s[8:9]
	s_lshl_b32 s1, s80, 5
	v_or_b32_e32 v77, s0, v88
	v_lshlrev_b32_e32 v4, 4, v93
	s_and_b32 s16, s1, 0x180
	v_mad_u64_u32 v[2:3], s[14:15], v77, s72, v[78:79]
	v_and_b32_e32 v80, 0x70, v4
	v_mov_b32_e32 v81, v71
	v_lshl_add_u64 v[2:3], v[2:3], 0, v[80:81]
	s_lshl_b32 s2, s16, 1
	v_lshl_add_u64 v[2:3], v[2:3], 0, s[2:3]
	global_load_dwordx4 v[6:9], v[2:3], off offset:1024
	global_load_dwordx4 v[10:13], v[2:3], off offset:1152
	s_lshl_b32 s1, s80, 6
	s_and_b32 s1, s1, 0xc0
	v_lshrrev_b32_e32 v2, 2, v93
	v_and_or_b32 v2, v2, 48, s1
	v_lshl_add_u32 v4, v92, 6, s16
	v_or3_b32 v72, v2, v89, s0
	v_ashrrev_i32_e32 v5, 31, v4
	v_mad_u64_u32 v[2:3], s[14:15], v72, s72, v[78:79]
	v_lshlrev_b64 v[74:75], 1, v[4:5]
	v_lshl_add_u64 v[2:3], v[2:3], 0, v[74:75]
	v_or_b32_e32 v14, 64, v77
	v_lshl_add_u64 v[22:23], v[2:3], 0, v[70:71]
	v_mad_u64_u32 v[14:15], s[14:15], v14, s72, v[78:79]
	global_load_dwordx4 v[2:5], v[22:23], off
	v_lshl_add_u64 v[14:15], v[14:15], 0, v[80:81]
	v_lshl_add_u64 v[18:19], v[14:15], 0, s[2:3]
	s_mov_b32 s100, 0x60000
	s_mov_b32 s101, 0
	v_lshl_add_u64 v[248:249], v[18:19], 0, s[100:101]
	global_load_dwordx4 v[14:17], v[18:19], off offset:1024
	s_nop 0
	global_load_dwordx4 v[18:21], v[18:19], off offset:1152
	global_load_dword v250, v[248:249], off offset:1024
	global_load_dword v251, v[248:249], off offset:1152
	s_nop 0
	global_load_dwordx4 v[50:53], v[22:23], off offset:64
	v_mul_u32_u24_e32 v22, 0x90, v88
	v_add3_u32 v73, 0, v22, v80
	v_or_b32_e32 v22, 0x80, v77
	v_add3_u32 v90, v86, v70, v87
	s_mov_b32 s1, s3
	v_cmp_lt_i32_e32 vcc, v83, v84
	s_waitcnt vmcnt(7)
	ds_write_b128 v73, v[6:9]
	s_waitcnt vmcnt(6)
	ds_write_b128 v73, v[10:13] offset:9216
	v_mad_u64_u32 v[10:11], s[14:15], v22, s72, v[78:79]
	v_lshl_add_u64 v[10:11], v[10:11], 0, v[80:81]
	v_lshl_add_u64 v[26:27], v[10:11], 0, s[2:3]
	s_waitcnt lgkmcnt(0)
	s_barrier
	ds_read_b128 v[6:9], v90
	ds_read_b128 v[10:13], v90 offset:2304
	v_lshl_add_u64 v[248:249], v[26:27], 0, s[100:101]
	global_load_dwordx4 v[22:25], v[26:27], off offset:1024
	global_load_dwordx4 v[30:33], v[26:27], off offset:1152
	global_load_dword v250, v[248:249], off offset:1024
	global_load_dword v251, v[248:249], off offset:1152
	ds_read_b128 v[26:29], v90 offset:64
	ds_read_b128 v[34:37], v90 offset:4608
	ds_read_b128 v[38:41], v90 offset:2368
	ds_read_b128 v[42:45], v90 offset:4672
	ds_read_b128 v[46:49], v90 offset:6912
	s_waitcnt vmcnt(9) lgkmcnt(6)
	v_mfma_f32_16x16x32_bf16 v[6:9], v[6:9], v[2:5], 0
	ds_read_b128 v[54:57], v90 offset:6976
	s_waitcnt vmcnt(8)
	ds_write_b128 v73, v[14:17] offset:18432
	s_waitcnt vmcnt(7)
	ds_write_b128 v73, v[18:21] offset:27648
	s_waitcnt lgkmcnt(0)
	v_mfma_f32_16x16x32_bf16 v[10:13], v[10:13], v[2:5], 0
	s_barrier
	v_mfma_f32_16x16x32_bf16 v[14:17], v[34:37], v[2:5], 0
	v_mfma_f32_16x16x32_bf16 v[18:21], v[46:49], v[2:5], 0
	ds_read_b128 v[34:37], v90 offset:18432
	ds_read_b128 v[46:49], v90 offset:18496
	ds_read_b128 v[58:61], v90 offset:20736
	ds_read_b128 v[94:97], v90 offset:20800
	s_waitcnt vmcnt(4)
	v_mfma_f32_16x16x32_bf16 v[62:65], v[26:29], v[50:53], v[6:9]
	s_nop 2
	v_or_b32_e32 v6, s16, v88
	s_waitcnt lgkmcnt(1)
	v_mfma_f32_16x16x32_bf16 v[98:101], v[58:61], v[2:5], 0
	ds_read_b128 v[58:61], v90 offset:23040
	ds_read_b128 v[102:105], v90 offset:23104
	v_mul_u32_u24_e32 v8, 0x9000, v6
	v_mov_b32_e32 v7, v71
	v_mfma_f32_16x16x32_bf16 v[66:69], v[38:41], v[50:53], v[10:13]
	v_mov_b32_e32 v9, v71
	s_nop 1
	v_lshl_add_u64 v[10:11], s[4:5], 0, v[80:81]
	v_or_b32_e32 v12, 64, v6
	v_or_b32_e32 v13, 0xc0, v77
	v_lshl_add_u64 v[10:11], s[0:1], 1, v[10:11]
	v_lshlrev_b32_e32 v6, 1, v8
	v_mul_u32_u24_e32 v8, 0x9000, v12
	v_mad_u64_u32 v[12:13], s[0:1], v13, s72, v[78:79]
	v_lshl_add_u64 v[78:79], v[10:11], 0, v[6:7]
	v_lshlrev_b32_e32 v8, 1, v8
	v_lshl_add_u64 v[6:7], v[12:13], 0, v[80:81]
	v_lshl_add_u64 v[80:81], v[10:11], 0, v[8:9]
	v_lshl_add_u64 v[10:11], v[6:7], 0, s[2:3]
	s_waitcnt lgkmcnt(1)
	v_mfma_f32_16x16x32_bf16 v[106:109], v[58:61], v[2:5], 0
	ds_read_b128 v[58:61], v90 offset:25344
	ds_read_b128 v[110:113], v90 offset:25408
	global_load_dwordx4 v[6:9], v[10:11], off offset:1024
	s_nop 0
	global_load_dwordx4 v[10:13], v[10:11], off offset:1152
	v_mul_f32_e32 v38, 0x3e000000, v68
	s_waitcnt lgkmcnt(1)
	v_mfma_f32_16x16x32_bf16 v[114:117], v[58:61], v[2:5], 0
	v_mul_f32_e32 v39, 0x3e000000, v69
	s_waitcnt vmcnt(5)
	ds_write_b128 v73, v[22:25]
	s_waitcnt vmcnt(4)
	ds_write_b128 v73, v[30:33] offset:9216
	v_mfma_f32_16x16x32_bf16 v[58:61], v[42:45], v[50:53], v[14:17]
	s_waitcnt lgkmcnt(0)
	s_barrier
; #define LAS __attribute__((address_space(3)))
; template <bool LOCAL>
; __device__ __forceinline__ void na_unit(const bf16* P, const bf16* VT, bf16* YCAT, const LAS float* rpb_l, LAS bf16* buf, int b, int gr, int hp, int qblk, int tid) {
;     ...
;                 const int cc = c - NLOC;
; #pragma unroll
;                 for (int t4 = 0; t4 < 4; ++t4) {
;                     const LAS bf16* kp = cb + (16 * t4 + fr) * 72 + 8 * fq;
;                     f32x4 acc = {0.f, 0.f, 0.f, 0.f};
;                     acc = __builtin_amdgcn_mfma_f32_16x16x32_bf16(*(const LAS bf16x8*)(kp), qf[0], acc, 0, 0, 0);
;                     acc = __builtin_amdgcn_mfma_f32_16x16x32_bf16(*(const LAS bf16x8*)(kp + 32), qf[1], acc, 0, 0, 0);
; #pragma unroll
;                     for (int e = 0; e < 4; ++e) { acc[e] *= 0.125f; m = fmaxf(m, acc[e]); }
;                     sc[4 * (cc >= 0 ? cc : 0) + t4] = acc; }
;             }
;             if (sidx == NCH - 1) { m = fmaxf(m, __shfl_xor(m, 16)); m = fmaxf(m, __shfl_xor(m, 32)); }
	s_nop 0
	v_mul_f32_e32 v14, 0x3e000000, v62
	v_mul_f32_e32 v15, 0x3e000000, v63
	v_mfma_f32_16x16x32_bf16 v[54:57], v[54:57], v[50:53], v[18:21]
	s_nop 1
	v_mul_f32_e32 v40, 0x3e000000, v58
	v_mul_f32_e32 v41, 0x3e000000, v59
	v_mul_f32_e32 v77, 0x3e000000, v60
	v_mfma_f32_16x16x32_bf16 v[42:45], v[94:97], v[50:53], v[98:101]
	v_mul_f32_e32 v18, 0x3e000000, v64
	v_mul_f32_e32 v19, 0x3e000000, v65
	v_mul_f32_e32 v20, 0x3e000000, v66
	v_max3_f32 v99, v14, s75, v15
	v_mul_f32_e32 v21, 0x3e000000, v67
	v_max3_f32 v18, v99, v18, v19
	v_mfma_f32_16x16x32_bf16 v[34:37], v[34:37], v[2:5], 0
	v_max3_f32 v18, v18, v20, v21
	ds_read_b128 v[14:17], v90
	v_max3_f32 v22, v18, v38, v39
	ds_read_b128 v[18:21], v90 offset:2304
	v_mul_f32_e32 v94, 0x3e000000, v61
	v_max3_f32 v22, v22, v40, v41
	v_mul_f32_e32 v95, 0x3e000000, v54
	v_mul_f32_e32 v96, 0x3e000000, v55
	v_max3_f32 v38, v22, v77, v94
	v_mfma_f32_16x16x32_bf16 v[46:49], v[46:49], v[50:53], v[34:37]
	v_mul_f32_e32 v97, 0x3e000000, v56
	v_mul_f32_e32 v98, 0x3e000000, v57
	v_max3_f32 v38, v38, v95, v96
	ds_read_b128 v[22:25], v90 offset:64
	ds_read_b128 v[30:33], v90 offset:4608
	v_max3_f32 v38, v38, v97, v98
	ds_read_b128 v[94:97], v90 offset:2368
	v_mfma_f32_16x16x32_bf16 v[34:37], v[102:105], v[50:53], v[106:109]
	v_mul_f32_e32 v100, 0x3e000000, v46
	v_mul_f32_e32 v101, 0x3e000000, v47
	v_mul_f32_e32 v102, 0x3e000000, v48
	v_mul_f32_e32 v103, 0x3e000000, v49
	v_max3_f32 v38, v38, v100, v101
	v_mul_f32_e32 v106, 0x3e000000, v42
	v_mul_f32_e32 v107, 0x3e000000, v43
	s_waitcnt lgkmcnt(4)
	v_mfma_f32_16x16x32_bf16 v[14:17], v[14:17], v[2:5], 0
	v_max3_f32 v38, v38, v102, v103
	v_mul_f32_e32 v108, 0x3e000000, v44
	v_mul_f32_e32 v109, 0x3e000000, v45
	s_waitcnt lgkmcnt(3)
	v_mfma_f32_16x16x32_bf16 v[18:21], v[18:21], v[2:5], 0
	ds_read_b128 v[98:101], v90 offset:4672
	s_waitcnt lgkmcnt(2)
	v_mfma_f32_16x16x32_bf16 v[102:105], v[30:33], v[2:5], 0
	v_max3_f32 v30, v38, v106, v107
	v_max3_f32 v30, v30, v108, v109
	v_mfma_f32_16x16x32_bf16 v[26:29], v[110:113], v[50:53], v[114:117]
	v_mul_f32_e32 v110, 0x3e000000, v34
	v_mul_f32_e32 v111, 0x3e000000, v35
	v_mul_f32_e32 v112, 0x3e000000, v36
	v_mul_f32_e32 v113, 0x3e000000, v37
	v_max3_f32 v30, v30, v110, v111
	v_mfma_f32_16x16x32_bf16 v[38:41], v[22:25], v[50:53], v[14:17]
	s_nop 1
	v_mul_f32_e32 v114, 0x3e000000, v26
	v_mul_f32_e32 v115, 0x3e000000, v27
	v_mul_f32_e32 v116, 0x3e000000, v28
	v_max3_f32 v14, v30, v112, v113
	s_waitcnt lgkmcnt(1)
	v_mfma_f32_16x16x32_bf16 v[30:33], v[94:97], v[50:53], v[18:21]
	v_lshl_add_u64 v[248:249], v[78:79], 0, 0
	v_lshl_add_u64 v[238:239], v[80:81], 0, 0
	global_load_dwordx4 v[94:97], v[78:79], off
	global_load_dwordx4 v[106:109], v[80:81], off
	global_load_dword v250, v[248:249], off offset:128
	global_load_dword v251, v[238:239], off offset:128
	v_mul_f32_e32 v117, 0x3e000000, v29
	v_max3_f32 v14, v14, v114, v115
	v_max3_f32 v22, v14, v116, v117
	ds_read_b128 v[14:17], v90 offset:6912
	v_mul_f32_e32 v23, 0x3e000000, v38
	v_mul_f32_e32 v24, 0x3e000000, v39
	v_mul_f32_e32 v25, 0x3e000000, v40
	v_mul_f32_e32 v77, 0x3e000000, v41
	v_max3_f32 v22, v22, v23, v24
	s_waitcnt lgkmcnt(1)
	v_mfma_f32_16x16x32_bf16 v[18:21], v[98:101], v[50:53], v[102:105]
	v_mul_f32_e32 v98, 0x3e000000, v30
	v_mul_f32_e32 v99, 0x3e000000, v31
	v_max3_f32 v22, v22, v25, v77
	v_max3_f32 v77, v22, v98, v99
	ds_read_b128 v[22:25], v90 offset:6976
	s_waitcnt vmcnt(5)
	ds_write_b128 v73, v[6:9] offset:18432
	s_waitcnt vmcnt(4)
	ds_write_b128 v73, v[10:13] offset:27648
	s_waitcnt lgkmcnt(0)
	s_barrier
	ds_read_b128 v[6:9], v90 offset:18432
	v_mul_f32_e32 v100, 0x3e000000, v32
	v_mul_f32_e32 v10, 0x3e000000, v33
	v_mfma_f32_16x16x32_bf16 v[14:17], v[14:17], v[2:5], 0
	v_max3_f32 v77, v77, v100, v10
	ds_read_b128 v[10:13], v90 offset:18496
	v_mul_f32_e32 v98, 0x3e000000, v18
	v_mfma_f32_16x16x32_bf16 v[22:25], v[22:25], v[50:53], v[14:17]
	v_mul_f32_e32 v99, 0x3e000000, v21
	ds_read_b128 v[110:113], v90 offset:25408
	s_nop 1
	v_mul_f32_e32 v14, 0x3e000000, v19
	v_max3_f32 v77, v77, v98, v14
	s_waitcnt lgkmcnt(2)
	v_mfma_f32_16x16x32_bf16 v[6:9], v[6:9], v[2:5], 0
	ds_read_b128 v[14:17], v90 offset:20736
	v_mul_f32_e32 v98, 0x3e000000, v20
	v_max3_f32 v77, v77, v98, v99
	s_waitcnt lgkmcnt(2)
	v_mfma_f32_16x16x32_bf16 v[10:13], v[10:13], v[50:53], v[6:9]
	v_mul_f32_e32 v98, 0x3e000000, v22
	v_mul_f32_e32 v99, 0x3e000000, v23
	v_max3_f32 v77, v77, v98, v99
	ds_read_b128 v[6:9], v90 offset:20800
	s_waitcnt lgkmcnt(1)
	v_mfma_f32_16x16x32_bf16 v[14:17], v[14:17], v[2:5], 0
	ds_read_b128 v[98:101], v90 offset:23040
	v_mul_f32_e32 v102, 0x3e000000, v24
	v_mul_f32_e32 v103, 0x3e000000, v25
	s_waitcnt lgkmcnt(1)
	v_mfma_f32_16x16x32_bf16 v[14:17], v[6:9], v[50:53], v[14:17]
	ds_read_b128 v[6:9], v90 offset:23104
	v_max3_f32 v77, v77, v102, v103
	ds_read_b128 v[102:105], v90 offset:25344
	s_waitcnt lgkmcnt(2)
	v_mfma_f32_16x16x32_bf16 v[98:101], v[98:101], v[2:5], 0
	v_mul_f32_e32 v114, 0x3e000000, v10
	v_mul_f32_e32 v115, 0x3e000000, v11
	v_mul_f32_e32 v116, 0x3e000000, v12
	s_waitcnt lgkmcnt(1)
	v_mfma_f32_16x16x32_bf16 v[6:9], v[6:9], v[50:53], v[98:101]
	v_mul_f32_e32 v117, 0x3e000000, v13
	v_max3_f32 v77, v77, v114, v115
	v_mul_f32_e32 v118, 0x3e000000, v14
	v_mul_f32_e32 v119, 0x3e000000, v15
	s_waitcnt lgkmcnt(0)
	v_mfma_f32_16x16x32_bf16 v[2:5], v[102:105], v[2:5], 0
	v_max3_f32 v77, v77, v116, v117
	v_mul_f32_e32 v90, 0x3e000000, v16
	v_mul_f32_e32 v98, 0x3e000000, v17
	v_max3_f32 v77, v77, v118, v119
	v_mul_f32_e32 v99, 0x3e000000, v6
	v_mul_f32_e32 v100, 0x3e000000, v7
	v_max3_f32 v77, v77, v90, v98
	v_mul_f32_e32 v101, 0x3e000000, v8
	v_mul_f32_e32 v102, 0x3e000000, v9
	v_max3_f32 v77, v77, v99, v100
	v_mfma_f32_16x16x32_bf16 v[2:5], v[110:113], v[50:53], v[2:5]
	v_max3_f32 v77, v77, v101, v102
	v_lshl_add_u64 v[248:249], v[78:79], 0, 0
	v_lshl_add_u64 v[238:239], v[80:81], 0, 0
	global_load_dwordx4 v[98:101], v[78:79], off offset:128
	global_load_dwordx4 v[102:105], v[80:81], off offset:128
	global_load_dword v250, v[248:249], off offset:256
	global_load_dword v251, v[238:239], off offset:256
	s_waitcnt vmcnt(7)
	ds_write_b128 v73, v[94:97]
	s_waitcnt vmcnt(6)
	ds_write_b128 v73, v[106:109] offset:9216
	s_nop 0
	v_mul_f32_e32 v50, 0x3e000000, v2
	v_mul_f32_e32 v51, 0x3e000000, v3
	v_mul_f32_e32 v52, 0x3e000000, v4
	v_mul_f32_e32 v53, 0x3e000000, v5
	v_max3_f32 v50, v77, v50, v51
	v_max3_f32 v51, v50, v52, v53
	v_cndmask_b32_e32 v50, v82, v83, vcc
	v_lshlrev_b32_e32 v50, 2, v50
	ds_bpermute_b32 v52, v50, v51
	v_cmp_lt_i32_e32 vcc, v85, v84
	s_waitcnt lgkmcnt(0)
	s_barrier
; #define LAS __attribute__((address_space(3)))
; __device__ __forceinline__ unsigned cvt_pk_bf16(float lo, float hi) { const float __attribute__((ext_vector_type(2))) v = {lo, hi}; return __builtin_bit_cast(unsigned, __builtin_convertvector(v, bf16x2_t)); }
; template <bool LOCAL>
; __device__ __forceinline__ void na_unit(const bf16* P, const bf16* VT, bf16* YCAT, const LAS float* rpb_l, LAS bf16* buf, int b, int gr, int hp, int qblk, int tid) {
;     ...
;             if (sidx == NCH - 1) { m = fmaxf(m, __shfl_xor(m, 16)); m = fmaxf(m, __shfl_xor(m, 32)); }
;         } else {
;             const int c = sidx - NCH;
;             if (LOCAL && c < 8) {
;                 float p[8];
; #pragma unroll
;                 for (int e = 0; e < 4; ++e) { p[e] = __expf(sl[2 * (c < 8 ? c : 0)][e] - m); p[4 + e] = __expf(sl[2 * (c < 8 ? c : 0) + 1][e] - m); }
; #pragma unroll
;                 for (int e = 0; e < 8; ++e) lsum += p[e];
;                 const bf16x8 pf = __builtin_bit_cast(bf16x8, (v4u){pg8::cvt_pk_bf16(p[0], p[1]), pg8::cvt_pk_bf16(p[2], p[3]), pg8::cvt_pk_bf16(p[4], p[5]), pg8::cvt_pk_bf16(p[6], p[7])});
; #pragma unroll
;                 for (int dt = 0; dt < 4; ++dt) { const LAS bf16* vp = cb + (16 * dt + fr) * 72 + kc0 + 4 * fq;
;                     o[dt] = __builtin_amdgcn_mfma_f32_16x16x32_bf16(frag44(vp, vp + 16), pf, o[dt], 0, 0, 0); }
;             } else {
;                 const int cc = c - NLOC;
; #pragma unroll
;                 for (int p2 = 0; p2 < 2; ++p2) {
;                     float p[8];
; #pragma unroll
;                     for (int e = 0; e < 4; ++e) { p[e] = __expf(sc[4 * (cc >= 0 ? cc : 0) + 2 * p2][e] - m); p[4 + e] = __expf(sc[4 * (cc >= 0 ? cc : 0) + 2 * p2 + 1][e] - m); }
; #pragma unroll
;                     for (int e = 0; e < 8; ++e) lsum += p[e];
;                     const bf16x8 pf = __builtin_bit_cast(bf16x8, (v4u){pg8::cvt_pk_bf16(p[0], p[1]), pg8::cvt_pk_bf16(p[2], p[3]), pg8::cvt_pk_bf16(p[4], p[5]), pg8::cvt_pk_bf16(p[6], p[7])});
; #pragma unroll
;                     for (int dt = 0; dt < 4; ++dt) { const LAS bf16* vp = cb + (16 * dt + fr) * 72 + 32 * p2 + 4 * fq;
;                         o[dt] = __builtin_amdgcn_mfma_f32_16x16x32_bf16(frag44(vp, vp + 16), pf, o[dt], 0, 0, 0); }
;                 }
	v_max_f32_e32 v52, v52, v52
	v_max_f32_e32 v52, v51, v52
	v_cndmask_b32_e32 v51, v82, v85, vcc
	v_lshlrev_b32_e32 v51, 2, v51
	ds_bpermute_b32 v53, v51, v52
	s_waitcnt lgkmcnt(0)
	v_max_f32_e32 v53, v53, v53
	v_max_f32_e32 v77, v52, v53
	v_fma_f32 v52, v62, s74, -v77
	v_fma_f32 v64, v64, s74, -v77
	v_mul_f32_e32 v52, 0x3fb8aa3b, v52
	v_fma_f32 v62, v63, s74, -v77
	v_mul_f32_e32 v64, 0x3fb8aa3b, v64
	v_fma_f32 v65, v65, s74, -v77
	v_exp_f32_e32 v53, v52
	v_fma_f32 v52, v66, s74, -v77
	v_mul_f32_e32 v62, 0x3fb8aa3b, v62
	v_exp_f32_e32 v66, v64
	v_fma_f32 v64, v68, s74, -v77
	v_mul_f32_e32 v65, 0x3fb8aa3b, v65
	v_add3_u32 v68, v86, v76, v87
	v_exp_f32_e32 v63, v62
	v_fma_f32 v62, v67, s74, -v77
	v_exp_f32_e32 v67, v65
	v_fma_f32 v65, v69, s74, -v77
	v_add_u32_e32 v69, 0x800, v68
	v_add_u32_e32 v90, 0x1000, v68
	v_add_u32_e32 v134, 0x1800, v68
	ds_read2_b64 v[94:97], v68 offset1:4
	ds_read2_b64 v[110:113], v69 offset0:32 offset1:36
	ds_read2_b64 v[114:117], v90 offset0:64 offset1:68
	ds_read2_b64 v[118:121], v134 offset0:96 offset1:100
	v_mul_f32_e32 v52, 0x3fb8aa3b, v52
	v_mul_f32_e32 v62, 0x3fb8aa3b, v62
	v_mul_f32_e32 v64, 0x3fb8aa3b, v64
	v_mul_f32_e32 v65, 0x3fb8aa3b, v65
	v_exp_f32_e32 v52, v52
	v_exp_f32_e32 v62, v62
	v_exp_f32_e32 v64, v64
	v_exp_f32_e32 v65, v65
	v_cvt_pk_bf16_f32 v106, v53, v63
	v_cvt_pk_bf16_f32 v107, v66, v67
	v_cvt_pk_bf16_f32 v108, v52, v62
	v_cvt_pk_bf16_f32 v109, v64, v65
	v_fma_f32 v58, v58, s74, -v77
	v_fma_f32 v54, v54, s74, -v77
	s_waitcnt lgkmcnt(3)
	v_mfma_f32_16x16x32_bf16 v[94:97], v[94:97], v[106:109], 0
	v_fma_f32 v59, v59, s74, -v77
	v_fma_f32 v55, v55, s74, -v77
	v_fma_f32 v60, v60, s74, -v77
	s_waitcnt lgkmcnt(2)
	v_mfma_f32_16x16x32_bf16 v[110:113], v[110:113], v[106:109], 0
	v_fma_f32 v56, v56, s74, -v77
	v_fma_f32 v61, v61, s74, -v77
	v_fma_f32 v57, v57, s74, -v77
	s_waitcnt lgkmcnt(1)
	v_mfma_f32_16x16x32_bf16 v[114:117], v[114:117], v[106:109], 0
	v_mul_f32_e32 v58, 0x3fb8aa3b, v58
	v_mul_f32_e32 v54, 0x3fb8aa3b, v54
	v_mul_f32_e32 v59, 0x3fb8aa3b, v59
	s_waitcnt lgkmcnt(0)
	v_mfma_f32_16x16x32_bf16 v[106:109], v[118:121], v[106:109], 0
	ds_read2_b64 v[118:121], v68 offset0:8 offset1:12
	v_mul_f32_e32 v55, 0x3fb8aa3b, v55
	v_mul_f32_e32 v60, 0x3fb8aa3b, v60
	v_mul_f32_e32 v56, 0x3fb8aa3b, v56
	v_mul_f32_e32 v61, 0x3fb8aa3b, v61
	v_mul_f32_e32 v57, 0x3fb8aa3b, v57
	v_exp_f32_e32 v58, v58
	v_exp_f32_e32 v54, v54
	v_exp_f32_e32 v59, v59
	v_exp_f32_e32 v55, v55
	v_exp_f32_e32 v60, v60
	v_exp_f32_e32 v56, v56
	v_exp_f32_e32 v61, v61
	v_exp_f32_e32 v57, v57
	v_cvt_pk_bf16_f32 v122, v58, v59
	v_cvt_pk_bf16_f32 v124, v54, v55
	v_cvt_pk_bf16_f32 v123, v60, v61
	v_cvt_pk_bf16_f32 v125, v56, v57
	v_fma_f32 v42, v42, s74, -v77
	v_mul_f32_e32 v42, 0x3fb8aa3b, v42
	s_waitcnt lgkmcnt(0)
	v_mfma_f32_16x16x32_bf16 v[94:97], v[118:121], v[122:125], v[94:97]
	ds_read2_b64 v[118:121], v69 offset0:40 offset1:44
	v_fma_f32 v46, v46, s74, -v77
	v_mul_f32_e32 v46, 0x3fb8aa3b, v46
	s_waitcnt lgkmcnt(0)
	v_mfma_f32_16x16x32_bf16 v[110:113], v[118:121], v[122:125], v[110:113]
	ds_read2_b64 v[118:121], v90 offset0:72 offset1:76
	v_add_u32_e32 v136, 0x5000, v68
	v_fma_f32 v26, v26, s74, -v77
	s_waitcnt lgkmcnt(0)
	v_mfma_f32_16x16x32_bf16 v[114:117], v[118:121], v[122:125], v[114:117]
	ds_read2_b64 v[118:121], v134 offset0:104 offset1:108
	v_lshl_add_u64 v[248:249], v[78:79], 0, 0
	v_lshl_add_u64 v[238:239], v[80:81], 0, 0
	global_load_dwordx4 v[126:129], v[78:79], off offset:256
	global_load_dwordx4 v[130:133], v[80:81], off offset:256
	global_load_dword v250, v[248:249], off offset:384
	global_load_dword v251, v[238:239], off offset:384
	s_waitcnt vmcnt(7)
	ds_write_b128 v73, v[98:101] offset:18432
	s_waitcnt vmcnt(6)
	ds_write_b128 v73, v[102:105] offset:27648
	s_waitcnt lgkmcnt(2)
	v_mfma_f32_16x16x32_bf16 v[106:109], v[118:121], v[122:125], v[106:109]
	v_exp_f32_e32 v119, v42
	v_fma_f32 v42, v47, s74, -v77
	v_mul_f32_e32 v42, 0x3fb8aa3b, v42
	v_exp_f32_e32 v120, v42
	v_fma_f32 v42, v43, s74, -v77
	v_mul_f32_e32 v42, 0x3fb8aa3b, v42
	v_exp_f32_e32 v121, v42
	v_fma_f32 v42, v48, s74, -v77
	v_mul_f32_e32 v42, 0x3fb8aa3b, v42
	v_exp_f32_e32 v122, v42
	v_fma_f32 v42, v44, s74, -v77
	v_mul_f32_e32 v42, 0x3fb8aa3b, v42
	v_add_u32_e32 v124, 0x4800, v68
	s_waitcnt lgkmcnt(0)
	s_barrier
; #define LAS __attribute__((address_space(3)))
; __device__ __forceinline__ unsigned cvt_pk_bf16(float lo, float hi) { const float __attribute__((ext_vector_type(2))) v = {lo, hi}; return __builtin_bit_cast(unsigned, __builtin_convertvector(v, bf16x2_t)); }
; #define NA_STORE(sidx) do { LAS bf16* d_ = buf + ((sidx) & 1) * 9216; _Pragma("unroll") for (int q_ = 0; q_ < 2; ++q_) *(LAS v4u*)(d_ + q_ * 4608 + lrow * 72 + lseg * 8) = ld[(sidx) & 1][q_]; } while (0)
; template <bool LOCAL>
; __device__ __forceinline__ void na_unit(const bf16* P, const bf16* VT, bf16* YCAT, const LAS float* rpb_l, LAS bf16* buf, int b, int gr, int hp, int qblk, int tid) {
;     ...
;             } else {
;                 const int cc = c - NLOC;
; #pragma unroll
;                 for (int p2 = 0; p2 < 2; ++p2) {
;                     float p[8];
; #pragma unroll
;                     for (int e = 0; e < 4; ++e) { p[e] = __expf(sc[4 * (cc >= 0 ? cc : 0) + 2 * p2][e] - m); p[4 + e] = __expf(sc[4 * (cc >= 0 ? cc : 0) + 2 * p2 + 1][e] - m); }
; #pragma unroll
;                     for (int e = 0; e < 8; ++e) lsum += p[e];
;                     const bf16x8 pf = __builtin_bit_cast(bf16x8, (v4u){pg8::cvt_pk_bf16(p[0], p[1]), pg8::cvt_pk_bf16(p[2], p[3]), pg8::cvt_pk_bf16(p[4], p[5]), pg8::cvt_pk_bf16(p[6], p[7])});
; #pragma unroll
;                     for (int dt = 0; dt < 4; ++dt) { const LAS bf16* vp = cb + (16 * dt + fr) * 72 + 32 * p2 + 4 * fq;
;                         o[dt] = __builtin_amdgcn_mfma_f32_16x16x32_bf16(frag44(vp, vp + 16), pf, o[dt], 0, 0, 0); }
;                 }
;             }
;         }
;         if (sidx + 1 < 2 * NCH) NA_STORE(sidx + 1);
	v_exp_f32_e32 v118, v46
	v_exp_f32_e32 v123, v42
	v_fma_f32 v42, v49, s74, -v77
	ds_read2_b64 v[46:49], v124 offset1:4
	v_mul_f32_e32 v42, 0x3fb8aa3b, v42
	v_exp_f32_e32 v125, v42
	v_fma_f32 v42, v45, s74, -v77
	v_mul_f32_e32 v42, 0x3fb8aa3b, v42
	v_exp_f32_e32 v135, v42
	v_cvt_pk_bf16_f32 v42, v118, v120
	v_cvt_pk_bf16_f32 v43, v122, v125
	v_cvt_pk_bf16_f32 v44, v119, v121
	v_cvt_pk_bf16_f32 v45, v123, v135
	v_mul_f32_e32 v26, 0x3fb8aa3b, v26
	v_fma_f32 v34, v34, s74, -v77
	s_waitcnt lgkmcnt(0)
	v_mfma_f32_16x16x32_bf16 v[46:49], v[46:49], v[42:45], v[94:97]
	v_mul_f32_e32 v34, 0x3fb8aa3b, v34
	v_fma_f32 v30, v30, s74, -v77
	v_mul_f32_e32 v30, 0x3fb8aa3b, v30
	ds_read2_b64 v[94:97], v136 offset0:32 offset1:36
	s_waitcnt lgkmcnt(0)
	v_mfma_f32_16x16x32_bf16 v[94:97], v[94:97], v[42:45], v[110:113]
	s_nop 2
	v_add_u32_e32 v110, 0x5800, v68
	v_add_u32_e32 v111, 0x6000, v68
	ds_read2_b64 v[98:101], v110 offset0:64 offset1:68
	ds_read2_b64 v[102:105], v111 offset0:96 offset1:100
	s_waitcnt lgkmcnt(1)
	v_mfma_f32_16x16x32_bf16 v[98:101], v[98:101], v[42:45], v[114:117]
	v_fma_f32 v38, v38, s74, -v77
	v_mul_f32_e32 v38, 0x3fb8aa3b, v38
	v_fma_f32 v18, v18, s74, -v77
	s_waitcnt lgkmcnt(0)
	v_mfma_f32_16x16x32_bf16 v[42:45], v[102:105], v[42:45], v[106:109]
	v_mul_f32_e32 v18, 0x3fb8aa3b, v18
	v_fma_f32 v10, v10, s74, -v77
	v_mul_f32_e32 v10, 0x3fb8aa3b, v10
	v_exp_f32_e32 v107, v26
	v_fma_f32 v26, v35, s74, -v77
	v_mul_f32_e32 v26, 0x3fb8aa3b, v26
	v_exp_f32_e32 v108, v26
	v_fma_f32 v26, v27, s74, -v77
	v_mul_f32_e32 v26, 0x3fb8aa3b, v26
	v_exp_f32_e32 v109, v26
	v_fma_f32 v26, v36, s74, -v77
	v_mul_f32_e32 v26, 0x3fb8aa3b, v26
	v_exp_f32_e32 v112, v26
	v_fma_f32 v26, v28, s74, -v77
	v_mul_f32_e32 v26, 0x3fb8aa3b, v26
	v_exp_f32_e32 v106, v34
	v_exp_f32_e32 v113, v26
	v_fma_f32 v26, v37, s74, -v77
	ds_read2_b64 v[34:37], v124 offset0:8 offset1:12
	v_mul_f32_e32 v26, 0x3fb8aa3b, v26
	v_exp_f32_e32 v114, v26
	v_fma_f32 v26, v29, s74, -v77
	v_mul_f32_e32 v26, 0x3fb8aa3b, v26
	v_exp_f32_e32 v115, v26
	v_cvt_pk_bf16_f32 v26, v106, v108
	v_cvt_pk_bf16_f32 v27, v112, v114
	v_cvt_pk_bf16_f32 v28, v107, v109
	v_cvt_pk_bf16_f32 v29, v113, v115
	v_fma_f32 v2, v2, s74, -v77
	v_mul_f32_e32 v2, 0x3fb8aa3b, v2
	s_waitcnt lgkmcnt(0)
	v_mfma_f32_16x16x32_bf16 v[34:37], v[34:37], v[26:29], v[46:49]
	v_fma_f32 v6, v6, s74, -v77
	v_mul_f32_e32 v6, 0x3fb8aa3b, v6
	s_nop 0
	ds_read2_b64 v[46:49], v136 offset0:40 offset1:44
	s_waitcnt lgkmcnt(0)
	v_mfma_f32_16x16x32_bf16 v[46:49], v[46:49], v[26:29], v[94:97]
	s_nop 2
	ds_read2_b64 v[94:97], v110 offset0:72 offset1:76
	s_waitcnt lgkmcnt(0)
	v_mfma_f32_16x16x32_bf16 v[94:97], v[94:97], v[26:29], v[98:101]
	s_nop 2
	ds_read2_b64 v[98:101], v111 offset0:104 offset1:108
	global_load_dwordx4 v[102:105], v[78:79], off offset:384
	s_nop 0
	global_load_dwordx4 v[78:81], v[80:81], off offset:384
	s_waitcnt vmcnt(5)
	ds_write_b128 v73, v[126:129]
	s_waitcnt vmcnt(4)
	ds_write_b128 v73, v[130:133] offset:9216
	s_waitcnt lgkmcnt(2)
	v_mfma_f32_16x16x32_bf16 v[26:29], v[98:101], v[26:29], v[42:45]
	v_exp_f32_e32 v99, v30
	v_fma_f32 v30, v39, s74, -v77
	v_mul_f32_e32 v30, 0x3fb8aa3b, v30
	v_exp_f32_e32 v100, v30
	v_fma_f32 v30, v31, s74, -v77
	v_mul_f32_e32 v30, 0x3fb8aa3b, v30
	v_exp_f32_e32 v101, v30
	v_fma_f32 v30, v40, s74, -v77
	v_mul_f32_e32 v30, 0x3fb8aa3b, v30
	v_exp_f32_e32 v116, v30
	v_fma_f32 v30, v32, s74, -v77
	v_mul_f32_e32 v30, 0x3fb8aa3b, v30
	s_waitcnt lgkmcnt(0)
	s_barrier
	v_exp_f32_e32 v98, v38
	v_exp_f32_e32 v117, v30
	v_fma_f32 v30, v41, s74, -v77
	ds_read2_b64 v[38:41], v68 offset1:4
	v_mul_f32_e32 v30, 0x3fb8aa3b, v30
	v_exp_f32_e32 v126, v30
	v_fma_f32 v30, v33, s74, -v77
	v_mul_f32_e32 v30, 0x3fb8aa3b, v30
	v_exp_f32_e32 v127, v30
	v_cvt_pk_bf16_f32 v30, v98, v100
	v_cvt_pk_bf16_f32 v31, v116, v126
	v_cvt_pk_bf16_f32 v32, v99, v101
	v_cvt_pk_bf16_f32 v33, v117, v127
	ds_read2_b64 v[42:45], v90 offset0:64 offset1:68
	s_waitcnt lgkmcnt(1)
	v_mfma_f32_16x16x32_bf16 v[34:37], v[38:41], v[30:33], v[34:37]
	ds_read2_b64 v[38:41], v69 offset0:32 offset1:36
	s_waitcnt lgkmcnt(0)
	v_mfma_f32_16x16x32_bf16 v[38:41], v[38:41], v[30:33], v[46:49]
	s_nop 2
	ds_read2_b64 v[46:49], v134 offset0:96 offset1:100
	s_waitcnt lgkmcnt(0)
	v_mfma_f32_16x16x32_bf16 v[26:29], v[46:49], v[30:33], v[26:29]
	v_exp_f32_e32 v46, v18
	v_fma_f32 v18, v22, s74, -v77
	v_mul_f32_e32 v18, 0x3fb8aa3b, v18
	v_exp_f32_e32 v47, v18
	v_fma_f32 v18, v19, s74, -v77
	v_mul_f32_e32 v18, 0x3fb8aa3b, v18
	v_exp_f32_e32 v48, v18
	v_fma_f32 v18, v23, s74, -v77
	v_mul_f32_e32 v18, 0x3fb8aa3b, v18
	v_exp_f32_e32 v49, v18
	v_fma_f32 v18, v20, s74, -v77
	v_mul_f32_e32 v18, 0x3fb8aa3b, v18
	v_mfma_f32_16x16x32_bf16 v[42:45], v[42:45], v[30:33], v[94:97]
	ds_read2_b64 v[30:33], v69 offset0:40 offset1:44
	s_nop 1
	v_exp_f32_e32 v94, v18
	v_fma_f32 v18, v24, s74, -v77
	v_mul_f32_e32 v18, 0x3fb8aa3b, v18
	v_exp_f32_e32 v95, v18
	v_fma_f32 v18, v21, s74, -v77
	v_mul_f32_e32 v22, 0x3fb8aa3b, v18
	ds_read2_b64 v[18:21], v68 offset0:8 offset1:12
	v_exp_f32_e32 v68, v22
	v_fma_f32 v22, v25, s74, -v77
	v_mul_f32_e32 v22, 0x3fb8aa3b, v22
	v_exp_f32_e32 v96, v22
	v_cvt_pk_bf16_f32 v22, v46, v48
	v_cvt_pk_bf16_f32 v23, v94, v68
	v_cvt_pk_bf16_f32 v24, v47, v49
	v_cvt_pk_bf16_f32 v25, v95, v96
	s_waitcnt lgkmcnt(0)
	s_nop 0
	v_mfma_f32_16x16x32_bf16 v[18:21], v[18:21], v[22:25], v[34:37]
	v_mfma_f32_16x16x32_bf16 v[30:33], v[30:33], v[22:25], v[38:41]
	s_nop 1
	ds_read2_b64 v[34:37], v90 offset0:72 offset1:76
	ds_read2_b64 v[38:41], v134 offset0:104 offset1:108
	s_waitcnt lgkmcnt(1)
	v_mfma_f32_16x16x32_bf16 v[34:37], v[34:37], v[22:25], v[42:45]
	s_waitcnt vmcnt(1)
	ds_write_b128 v73, v[102:105] offset:18432
	s_waitcnt vmcnt(0)
	ds_write_b128 v73, v[78:81] offset:27648
	s_waitcnt lgkmcnt(0)
	s_barrier
; #define LAS __attribute__((address_space(3)))
; __device__ __forceinline__ unsigned cvt_pk_bf16(float lo, float hi) { const float __attribute__((ext_vector_type(2))) v = {lo, hi}; return __builtin_bit_cast(unsigned, __builtin_convertvector(v, bf16x2_t)); }
; #define NA_STORE(sidx) do { LAS bf16* d_ = buf + ((sidx) & 1) * 9216; _Pragma("unroll") for (int q_ = 0; q_ < 2; ++q_) *(LAS v4u*)(d_ + q_ * 4608 + lrow * 72 + lseg * 8) = ld[(sidx) & 1][q_]; } while (0)
; template <bool LOCAL>
; __device__ __forceinline__ void na_unit(const bf16* P, const bf16* VT, bf16* YCAT, const LAS float* rpb_l, LAS bf16* buf, int b, int gr, int hp, int qblk, int tid) {
;     ...
;             } else {
;                 const int cc = c - NLOC;
; #pragma unroll
;                 for (int p2 = 0; p2 < 2; ++p2) {
;                     float p[8];
; #pragma unroll
;                     for (int e = 0; e < 4; ++e) { p[e] = __expf(sc[4 * (cc >= 0 ? cc : 0) + 2 * p2][e] - m); p[4 + e] = __expf(sc[4 * (cc >= 0 ? cc : 0) + 2 * p2 + 1][e] - m); }
; #pragma unroll
;                     for (int e = 0; e < 8; ++e) lsum += p[e];
;                     const bf16x8 pf = __builtin_bit_cast(bf16x8, (v4u){pg8::cvt_pk_bf16(p[0], p[1]), pg8::cvt_pk_bf16(p[2], p[3]), pg8::cvt_pk_bf16(p[4], p[5]), pg8::cvt_pk_bf16(p[6], p[7])});
; #pragma unroll
;                     for (int dt = 0; dt < 4; ++dt) { const LAS bf16* vp = cb + (16 * dt + fr) * 72 + 32 * p2 + 4 * fq;
;                         o[dt] = __builtin_amdgcn_mfma_f32_16x16x32_bf16(frag44(vp, vp + 16), pf, o[dt], 0, 0, 0); }
;                 }
;             }
;         }
;         if (sidx + 1 < 2 * NCH) NA_STORE(sidx + 1);
;         __syncthreads();
;     }
;     ...
;     lsum += __shfl_xor(lsum, 16); lsum += __shfl_xor(lsum, 32);
;     const float inv = 1.f / lsum;
;     bf16* op = YCAT + (size_t)(qrow0 + fr) * D + 512 + h * 64 + 4 * fq;
; #pragma unroll
;     for (int dt = 0; dt < 4; ++dt) { v2u w; w.x = pg8::cvt_pk_bf16(o[dt][0] * inv, o[dt][1] * inv); w.y = pg8::cvt_pk_bf16(o[dt][2] * inv, o[dt][3] * inv); *(v2u*)(op + dt * 16) = w; }
	v_mfma_f32_16x16x32_bf16 v[22:25], v[38:41], v[22:25], v[26:29]
	v_exp_f32_e32 v38, v10
	v_fma_f32 v10, v14, s74, -v77
	v_mul_f32_e32 v10, 0x3fb8aa3b, v10
	v_exp_f32_e32 v39, v10
	v_fma_f32 v10, v11, s74, -v77
	v_mul_f32_e32 v10, 0x3fb8aa3b, v10
	v_exp_f32_e32 v40, v10
	v_fma_f32 v10, v15, s74, -v77
	v_mul_f32_e32 v10, 0x3fb8aa3b, v10
	v_exp_f32_e32 v41, v10
	v_fma_f32 v10, v12, s74, -v77
	v_mul_f32_e32 v10, 0x3fb8aa3b, v10
	v_exp_f32_e32 v42, v10
	v_fma_f32 v10, v16, s74, -v77
	v_mul_f32_e32 v10, 0x3fb8aa3b, v10
	v_exp_f32_e32 v43, v10
	v_fma_f32 v10, v13, s74, -v77
	ds_read2_b64 v[26:29], v110 offset0:64 offset1:68
	v_mul_f32_e32 v14, 0x3fb8aa3b, v10
	v_exp_f32_e32 v44, v14
	v_fma_f32 v14, v17, s74, -v77
	v_mul_f32_e32 v14, 0x3fb8aa3b, v14
	v_exp_f32_e32 v45, v14
	v_cvt_pk_bf16_f32 v14, v38, v40
	v_cvt_pk_bf16_f32 v15, v42, v44
	v_cvt_pk_bf16_f32 v16, v39, v41
	v_cvt_pk_bf16_f32 v17, v43, v45
	ds_read2_b64 v[10:13], v124 offset1:4
	v_mov_b32_e32 v73, v71
	s_waitcnt lgkmcnt(1)
	v_mfma_f32_16x16x32_bf16 v[26:29], v[26:29], v[14:17], v[34:37]
	s_nop 2
	v_add_f32_e32 v34, 0, v53
	v_add_f32_e32 v34, v63, v34
	v_add_f32_e32 v34, v66, v34
	v_add_f32_e32 v34, v67, v34
	v_add_f32_e32 v34, v52, v34
	v_add_f32_e32 v34, v62, v34
	v_add_f32_e32 v34, v64, v34
	v_add_f32_e32 v34, v65, v34
	v_add_f32_e32 v34, v58, v34
	v_add_f32_e32 v34, v59, v34
	v_add_f32_e32 v34, v60, v34
	v_add_f32_e32 v34, v61, v34
	v_add_f32_e32 v34, v54, v34
	v_add_f32_e32 v34, v55, v34
	v_add_f32_e32 v34, v56, v34
	v_add_f32_e32 v34, v57, v34
	s_waitcnt lgkmcnt(0)
	v_mfma_f32_16x16x32_bf16 v[10:13], v[10:13], v[14:17], v[18:21]
	v_add_f32_e32 v34, v118, v34
	v_add_f32_e32 v34, v120, v34
	v_add_f32_e32 v34, v122, v34
	ds_read2_b64 v[18:21], v136 offset0:32 offset1:36
	v_add_f32_e32 v34, v125, v34
	v_add_f32_e32 v34, v119, v34
	v_add_f32_e32 v34, v121, v34
	v_add_f32_e32 v34, v123, v34
	v_add_f32_e32 v34, v135, v34
	v_add_f32_e32 v34, v106, v34
	s_waitcnt lgkmcnt(0)
	v_mfma_f32_16x16x32_bf16 v[18:21], v[18:21], v[14:17], v[30:33]
	v_add_f32_e32 v34, v108, v34
	s_nop 1
	ds_read2_b64 v[30:33], v111 offset0:96 offset1:100
	v_add_f32_e32 v34, v112, v34
	v_add_f32_e32 v34, v114, v34
	v_add_f32_e32 v34, v107, v34
	v_add_f32_e32 v34, v109, v34
	v_add_f32_e32 v34, v113, v34
	v_add_f32_e32 v34, v115, v34
	v_add_f32_e32 v34, v98, v34
	v_add_f32_e32 v34, v100, v34
	s_waitcnt lgkmcnt(0)
	v_mfma_f32_16x16x32_bf16 v[14:17], v[30:33], v[14:17], v[22:25]
	v_add_f32_e32 v34, v116, v34
	v_add_f32_e32 v34, v126, v34
	v_add_f32_e32 v34, v99, v34
	v_exp_f32_e32 v23, v2
	v_fma_f32 v2, v7, s74, -v77
	v_mul_f32_e32 v2, 0x3fb8aa3b, v2
	v_exp_f32_e32 v24, v2
	v_fma_f32 v2, v3, s74, -v77
	v_mul_f32_e32 v2, 0x3fb8aa3b, v2
	v_add_f32_e32 v34, v101, v34
	v_exp_f32_e32 v25, v2
	v_fma_f32 v2, v8, s74, -v77
	v_add_f32_e32 v34, v117, v34
	v_mul_f32_e32 v2, 0x3fb8aa3b, v2
	v_add_f32_e32 v34, v127, v34
	v_exp_f32_e32 v30, v2
	v_fma_f32 v2, v4, s74, -v77
	v_add_f32_e32 v34, v46, v34
	v_mul_f32_e32 v2, 0x3fb8aa3b, v2
	v_add_f32_e32 v34, v48, v34
	v_exp_f32_e32 v22, v6
	v_exp_f32_e32 v31, v2
	v_fma_f32 v2, v9, s74, -v77
	ds_read2_b64 v[6:9], v124 offset0:8 offset1:12
	v_add_f32_e32 v34, v94, v34
	v_mul_f32_e32 v2, 0x3fb8aa3b, v2
	v_add_f32_e32 v34, v68, v34
	v_exp_f32_e32 v32, v2
	v_fma_f32 v2, v5, s74, -v77
	v_add_f32_e32 v34, v47, v34
	v_mul_f32_e32 v2, 0x3fb8aa3b, v2
	v_add_f32_e32 v34, v49, v34
	v_exp_f32_e32 v33, v2
	v_add_f32_e32 v34, v95, v34
	v_add_f32_e32 v34, v96, v34
	v_add_f32_e32 v34, v38, v34
	v_add_f32_e32 v34, v40, v34
	v_cvt_pk_bf16_f32 v2, v22, v24
	v_cvt_pk_bf16_f32 v3, v30, v32
	v_cvt_pk_bf16_f32 v4, v23, v25
	v_cvt_pk_bf16_f32 v5, v31, v33
	v_add_f32_e32 v34, v42, v34
	v_add_f32_e32 v34, v44, v34
	s_waitcnt lgkmcnt(0)
	v_mfma_f32_16x16x32_bf16 v[6:9], v[6:9], v[2:5], v[10:13]
	v_add_f32_e32 v34, v39, v34
	v_add_f32_e32 v34, v41, v34
	v_add_f32_e32 v34, v43, v34
	ds_read2_b64 v[10:13], v136 offset0:40 offset1:44
	v_add_f32_e32 v34, v45, v34
	v_add_f32_e32 v22, v22, v34
	v_add_f32_e32 v22, v24, v22
	v_add_f32_e32 v22, v30, v22
	v_add_f32_e32 v22, v32, v22
	s_waitcnt lgkmcnt(0)
	v_mfma_f32_16x16x32_bf16 v[10:13], v[10:13], v[2:5], v[18:21]
	s_nop 2
	ds_read2_b64 v[18:21], v110 offset0:72 offset1:76
	v_add_f32_e32 v22, v23, v22
	v_add_f32_e32 v22, v25, v22
	v_add_f32_e32 v22, v31, v22
	v_add_f32_e32 v30, v33, v22
	ds_bpermute_b32 v31, v50, v30
	ds_read2_b64 v[22:25], v111 offset0:104 offset1:108
	s_waitcnt lgkmcnt(2)
	v_mfma_f32_16x16x32_bf16 v[18:21], v[18:21], v[2:5], v[26:29]
	v_mov_b32_e32 v77, v71
	s_waitcnt lgkmcnt(1)
	s_nop 0
	v_add_f32_e32 v26, v30, v31
	ds_bpermute_b32 v27, v51, v26
	s_waitcnt lgkmcnt(1)
	v_mfma_f32_16x16x32_bf16 v[14:17], v[22:25], v[2:5], v[14:17]
	s_waitcnt lgkmcnt(0)
	v_add_f32_e32 v2, v26, v27
	v_div_scale_f32 v3, s[0:1], v2, v2, 1.0
	v_rcp_f32_e32 v4, v3
	s_barrier
	s_mov_b64 s[0:1], 0
	v_fma_f32 v5, -v3, v4, 1.0
	v_fmac_f32_e32 v4, v5, v4
	v_div_scale_f32 v5, vcc, 1.0, v2, 1.0
	v_mul_f32_e32 v22, v5, v4
	v_fma_f32 v23, -v3, v22, v5
	v_fmac_f32_e32 v22, v23, v4
	v_fma_f32 v3, -v3, v22, v5
	v_div_fmas_f32 v3, v3, v4, v22
	v_div_fixup_f32 v22, v3, v2, 1.0
	v_lshlrev_b64 v[2:3], 11, v[72:73]
	v_lshl_add_u64 v[2:3], s[10:11], 0, v[2:3]
	v_lshl_add_u64 v[2:3], v[2:3], 0, v[74:75]
	v_pk_mul_f32 v[6:7], v[6:7], v[22:23] op_sel_hi:[1,0]
	v_pk_mul_f32 v[8:9], v[8:9], v[22:23] op_sel_hi:[1,0]
	v_lshl_add_u64 v[4:5], v[2:3], 0, v[76:77]
	v_cvt_pk_bf16_f32 v6, v6, v7
	v_cvt_pk_bf16_f32 v7, v8, v9
	global_store_dwordx2 v[4:5], v[6:7], off offset:1024
	v_pk_mul_f32 v[6:7], v[10:11], v[22:23] op_sel_hi:[1,0]
	v_pk_mul_f32 v[8:9], v[12:13], v[22:23] op_sel_hi:[1,0]
	v_cvt_pk_bf16_f32 v6, v6, v7
	v_cvt_pk_bf16_f32 v7, v8, v9
	global_store_dwordx2 v[4:5], v[6:7], off offset:1056
	v_pk_mul_f32 v[6:7], v[18:19], v[22:23] op_sel_hi:[1,0]
	v_pk_mul_f32 v[8:9], v[20:21], v[22:23] op_sel_hi:[1,0]
	v_cvt_pk_bf16_f32 v6, v6, v7
	v_cvt_pk_bf16_f32 v7, v8, v9
	v_lshl_add_u64 v[2:3], v[4:5], 0, s[12:13]
	global_store_dwordx2 v[4:5], v[6:7], off offset:1088
	v_pk_mul_f32 v[4:5], v[14:15], v[22:23] op_sel_hi:[1,0]
	v_pk_mul_f32 v[6:7], v[16:17], v[22:23] op_sel_hi:[1,0]
	v_cvt_pk_bf16_f32 v4, v4, v5

; #define LAS __attribute__((address_space(3)))
; template <bool LOCAL>
; __device__ __forceinline__ void na_unit(const bf16* P, const bf16* VT, bf16* YCAT, const LAS float* rpb_l, LAS bf16* buf, int b, int gr, int hp, int qblk, int tid) {
;     ...
;     const int lane = tid & 63, wv = tid >> 6, fr = lane & 15, fq = lane >> 4, hh = wv >> 2, qb = wv & 3, h = 2 * hp + hh;
;     const int qrow0 = LOCAL ? NCTX + b * SEQ + gr * 64 + 16 * qb : b * CTXL + qblk * 64 + 16 * qb;
;     const int r0 = min(max(gr - 4, 0), 24);
;     const int kc0 = qb == 0 ? 0 : qb == 1 ? 8 : qb == 2 ? 24 : 32;
;     const int qcol = 16 * qb + fr, cs = min(max(qcol - 8, 0), 48);
;     const LAS float* rpb = rpb_l + h * 15 * 31;
;     v4u ld[2][2];
;     const int lrow = (tid >> 3) & 63, lseg = tid & 7;
;     ...
;     bf16x8 qf[2];
; #pragma unroll
;     for (int ks = 0; ks < 2; ++ks) qf[ks] = *(const bf16x8*)(P + (size_t)(qrow0 + fr) * DINP + h * 64 + 32 * ks + 8 * fq);
;     f32x4 sl[16], sc[16];
;     float m = -1.0e30f, lsum = 0.f;
;     f32x4 o[4];
; #pragma unroll
;     for (int dt = 0; dt < 4; ++dt) o[dt] = (f32x4){0.f, 0.f, 0.f, 0.f};
;     NA_ISSUE(0); NA_ISSUE(1); NA_STORE(0);
;     __syncthreads();
; #pragma unroll
;     for (int sidx = 0; sidx < 2 * NCH; ++sidx) {
;         if (sidx + 2 < 2 * NCH) NA_ISSUE(sidx + 2);
;         const LAS bf16* cb = buf + (sidx & 1) * 9216 + hh * 4608;
;         if (sidx < NCH) {
;             const int c = sidx;
;             if (LOCAL && c < 8) {
; #pragma unroll
;                 for (int t2 = 0; t2 < 2; ++t2) {
;                     const LAS bf16* kp = cb + (kc0 + 16 * t2 + fr) * 72 + 8 * fq;
;                     f32x4 acc = {0.f, 0.f, 0.f, 0.f};
;                     acc = __builtin_amdgcn_mfma_f32_16x16x32_bf16(*(const LAS bf16x8*)(kp), qf[0], acc, 0, 0, 0);
;                     acc = __builtin_amdgcn_mfma_f32_16x16x32_bf16(*(const LAS bf16x8*)(kp + 32), qf[1], acc, 0, 0, 0);
;                     const LAS float* rb = rpb + (r0 + c - gr + 7) * 31 + 15 - qcol;
; #pragma unroll
;                     for (int e = 0; e < 4; ++e) { const int kcol = kc0 + 16 * t2 + 4 * fq + e; const bool ok = (kcol >= cs) && (kcol < cs + 16);
;                         const float sv = ok ? acc[e] * 0.125f + rb[ok ? kcol : qcol] : -1.0e30f; acc[e] = sv; m = fmaxf(m, sv); }
;                     sl[2 * (c < 8 ? c : 0) + t2] = acc; }
.LBB0_2898:
	s_or_b64 exec, exec, s[0:1]
	s_bfe_u32 s19, s80, 0x50002
	v_sub_u32_e64 v3, s19, 4 clamp
	s_ashr_i32 s17, s80, 7
	v_readfirstlane_b32 s0, v3
	s_lshl_b32 s26, s17, 11
	s_min_u32 s20, s0, 24
	s_add_i32 s14, s26, 0x1000
	s_lshl_b32 s15, s20, 6
	s_or_b32 s16, s15, s14
	v_mov_b64_e32 v[18:19], s[8:9]
	v_and_b32_e32 v32, 7, v93
	v_or_b32_e32 v3, s16, v88
	s_and_b32 s18, s80, 3
	v_mad_i64_i32 v[4:5], s[0:1], v3, s72, v[18:19]
	v_lshlrev_b32_e32 v26, 4, v32
	v_mov_b32_e32 v27, v71
	v_lshl_add_u64 v[4:5], v[4:5], 0, v[26:27]
	s_lshl_b32 s2, s18, 8
	v_lshl_add_u64 v[4:5], v[4:5], 0, s[2:3]
	global_load_dwordx4 v[10:13], v[4:5], off offset:1024
	global_load_dwordx4 v[14:17], v[4:5], off offset:1152
	s_lshl_b32 s0, s19, 6
	v_lshl_or_b32 v31, v2, 4, v89
	v_lshl_add_u32 v33, s18, 1, v92
	s_or_b32 s0, s14, s0
	v_mad_u32_u24 v2, v88, s73, 0
	v_lshlrev_b32_e32 v72, 6, v33
	s_add_i32 s50, s26, 0x1040
	v_or_b32_e32 v74, s0, v31
	v_add_u32_e32 v75, v2, v26
	v_ashrrev_i32_e32 v73, 31, v72
	v_or_b32_e32 v4, s50, v88
	v_mad_i64_i32 v[2:3], s[0:1], v74, s72, v[18:19]
	v_add_u32_e32 v4, s15, v4
	v_lshl_add_u64 v[2:3], v[72:73], 1, v[2:3]
	v_mad_i64_i32 v[4:5], s[0:1], v4, s72, v[18:19]
	v_lshl_add_u64 v[2:3], v[2:3], 0, v[70:71]
	v_lshl_add_u64 v[20:21], v[4:5], 0, v[26:27]
	global_load_dwordx4 v[6:9], v[2:3], off
	s_nop 0
	global_load_dwordx4 v[2:5], v[2:3], off offset:64
	s_or_b32 s14, s26, s15
	s_addk_i32 s14, 0x1080
	v_or_b32_e32 v24, s14, v88
	v_mad_i64_i32 v[28:29], s[0:1], v24, s72, v[18:19]
	v_lshl_add_u64 v[26:27], v[28:29], 0, v[26:27]
	v_lshl_add_u64 v[22:23], v[20:21], 0, s[2:3]
	v_lshl_add_u64 v[26:27], v[26:27], 0, s[2:3]
	s_mov_b32 s100, 0x60000
	s_mov_b32 s101, 0
	v_lshl_add_u64 v[248:249], v[22:23], 0, s[100:101]
	global_load_dwordx4 v[18:21], v[22:23], off offset:1024
	s_nop 0
	global_load_dwordx4 v[22:25], v[22:23], off offset:1152
	global_load_dword v250, v[248:249], off offset:1024
	global_load_dword v251, v[248:249], off offset:1152
	v_add_u32_e32 v30, v86, v70
	v_add_u32_e32 v34, v90, v89
	v_mad_u32_u24 v36, v34, s73, v30
	s_movk_i32 s0, 0x744
	v_mul_lo_u32 v33, v33, s0
	s_sub_i32 s0, s20, s19
	s_mulk_i32 s0, 0x7c
	v_sub_u32_e64 v35, v31, 8 clamp
	s_add_i32 s0, s0, 0
	v_min_u32_e32 v35, 48, v35
	v_lshlrev_b32_e32 v77, 2, v91
	v_add_u32_e32 v33, s0, v33
	v_lshlrev_b32_e32 v31, 2, v31
	v_sub_u32_e32 v31, v33, v31
	v_add_u32_e32 v33, v90, v77
	v_cmp_ge_u32_e32 vcc, v33, v35
	v_mov_b32_e32 v91, 0xf149f2ca
	v_lshl_add_u32 v31, v33, 2, v31
	v_mov_b32_e32 v92, 0xf149f2ca
	s_waitcnt vmcnt(7)
	ds_write_b128 v75, v[10:13]
	s_waitcnt vmcnt(6)
	ds_write_b128 v75, v[14:17] offset:9216
	s_waitcnt lgkmcnt(0)
	s_barrier
	ds_read_b32 v240, v31 offset:37792
	ds_read_b32 v241, v31 offset:37796
	ds_read_b32 v242, v31 offset:37800
	ds_read_b32 v243, v31 offset:37804
	ds_read_b32 v244, v31 offset:37856
	ds_read_b32 v245, v31 offset:37860
	ds_read_b32 v246, v31 offset:37864
	ds_read_b32 v247, v31 offset:37868
	v_lshl_add_u64 v[248:249], v[26:27], 0, s[100:101]
	global_load_dwordx4 v[10:13], v[26:27], off offset:1024
	global_load_dwordx4 v[14:17], v[26:27], off offset:1152
	global_load_dword v250, v[248:249], off offset:1024
	global_load_dword v251, v[248:249], off offset:1152
	ds_read_b128 v[26:29], v36
	ds_read_b128 v[38:41], v36 offset:64
	s_waitcnt vmcnt(9) lgkmcnt(1)
	v_mfma_f32_16x16x32_bf16 v[26:29], v[26:29], v[6:9], 0
	v_add_u32_e32 v36, 16, v35
	v_cmp_lt_u32_e64 s[0:1], v33, v36
	s_and_b64 s[28:29], vcc, s[0:1]
	s_waitcnt vmcnt(8) lgkmcnt(0)
	v_mfma_f32_16x16x32_bf16 v[26:29], v[38:41], v[2:5], v[26:29]
	s_nop 2
	s_waitcnt lgkmcnt(0)
	s_nop 3
	v_fmac_f32_e32 v240, 0x3e000000, v26
	v_cndmask_b32_e64 v92, v92, v240, s[28:29]
	s_nop 4
	v_or_b32_e32 v26, 1, v33
	v_cmp_ge_u32_e32 vcc, v26, v35
	v_cmp_lt_u32_e64 s[0:1], v26, v36
	s_and_b64 s[30:31], vcc, s[0:1]
	s_nop 2
	s_waitcnt lgkmcnt(0)
	v_fmac_f32_e32 v241, 0x3e000000, v27
	v_cndmask_b32_e64 v91, v91, v241, s[30:31]
	v_or_b32_e32 v26, 2, v33
	v_cmp_ge_u32_e32 vcc, v26, v35
	v_cmp_lt_u32_e64 s[0:1], v26, v36
	s_and_b64 s[34:35], vcc, s[0:1]
	v_mov_b32_e32 v93, 0xf149f2ca
	v_mov_b32_e32 v94, 0xf149f2ca
	s_nop 2
	s_waitcnt lgkmcnt(0)
	v_fmac_f32_e32 v242, 0x3e000000, v28
	v_cndmask_b32_e64 v94, v94, v242, s[34:35]
	v_or_b32_e32 v26, 3, v33
	v_cmp_ge_u32_e32 vcc, v26, v35
	v_cmp_lt_u32_e64 s[0:1], v26, v36
	s_and_b64 s[36:37], vcc, s[0:1]
	s_nop 2
	s_waitcnt lgkmcnt(0)
	v_fmac_f32_e32 v243, 0x3e000000, v29
	v_cndmask_b32_e64 v93, v93, v243, s[36:37]
	v_add_u32_e32 v37, 16, v90
	v_add_u32_e32 v33, v37, v89
	v_mad_u32_u24 v38, v33, s73, v30
	ds_read_b128 v[26:29], v38
	ds_read_b128 v[38:41], v38 offset:64
	v_add_u32_e32 v37, v37, v77
	v_cmp_ge_u32_e32 vcc, v37, v35
	v_cmp_lt_u32_e64 s[0:1], v37, v36
	s_waitcnt lgkmcnt(1)
	v_mfma_f32_16x16x32_bf16 v[26:29], v[26:29], v[6:9], 0
	s_and_b64 s[38:39], vcc, s[0:1]
	v_mov_b32_e32 v95, 0xf149f2ca
	v_mov_b32_e32 v96, 0xf149f2ca
	s_waitcnt lgkmcnt(0)
	v_mfma_f32_16x16x32_bf16 v[26:29], v[38:41], v[2:5], v[26:29]
	s_nop 2
	s_waitcnt lgkmcnt(0)
	s_nop 3
	v_fmac_f32_e32 v244, 0x3e000000, v26
	v_cndmask_b32_e64 v96, v96, v244, s[38:39]
	s_nop 4
	v_or_b32_e32 v26, 1, v37
	v_cmp_ge_u32_e32 vcc, v26, v35
	v_cmp_lt_u32_e64 s[0:1], v26, v36
	s_and_b64 s[44:45], vcc, s[0:1]
	s_nop 2
	s_waitcnt lgkmcnt(0)
	v_fmac_f32_e32 v245, 0x3e000000, v27
	v_cndmask_b32_e64 v95, v95, v245, s[44:45]
	v_or_b32_e32 v26, 2, v37
	v_cmp_ge_u32_e32 vcc, v26, v35
	v_cmp_lt_u32_e64 s[0:1], v26, v36
	s_and_b64 s[46:47], vcc, s[0:1]
	v_mov_b32_e32 v97, 0xf149f2ca
	v_mov_b32_e32 v99, 0xf149f2ca
	s_nop 2
	s_waitcnt lgkmcnt(0)
	v_fmac_f32_e32 v246, 0x3e000000, v28
	v_cndmask_b32_e64 v99, v99, v246, s[46:47]
	v_or_b32_e32 v26, 3, v37
	v_cmp_ge_u32_e32 vcc, v26, v35
	v_cmp_lt_u32_e64 s[0:1], v26, v36
	s_and_b64 s[66:67], vcc, s[0:1]
	s_nop 2
	s_waitcnt lgkmcnt(0)
	v_fmac_f32_e32 v247, 0x3e000000, v29
	v_cndmask_b32_e64 v97, v97, v247, s[66:67]
	v_mul_u32_u24_e32 v27, 0x90, v34
	v_lshlrev_b32_e32 v26, 3, v32
	v_add_u32_e32 v32, v30, v27
	s_waitcnt vmcnt(7)
	ds_write_b128 v75, v[18:21] offset:18432
	s_waitcnt vmcnt(6)
	ds_write_b128 v75, v[22:25] offset:27648
	s_waitcnt lgkmcnt(0)
	s_barrier
; #define LAS __attribute__((address_space(3)))
; template <bool LOCAL>
; __device__ __forceinline__ void na_unit(const bf16* P, const bf16* VT, bf16* YCAT, const LAS float* rpb_l, LAS bf16* buf, int b, int gr, int hp, int qblk, int tid) {
;     ...
;     for (int sidx = 0; sidx < 2 * NCH; ++sidx) {
;         if (sidx + 2 < 2 * NCH) NA_ISSUE(sidx + 2);
;         const LAS bf16* cb = buf + (sidx & 1) * 9216 + hh * 4608;
;         if (sidx < NCH) {
;             const int c = sidx;
;             if (LOCAL && c < 8) {
; #pragma unroll
;                 for (int t2 = 0; t2 < 2; ++t2) {
;                     const LAS bf16* kp = cb + (kc0 + 16 * t2 + fr) * 72 + 8 * fq;
;                     f32x4 acc = {0.f, 0.f, 0.f, 0.f};
;                     acc = __builtin_amdgcn_mfma_f32_16x16x32_bf16(*(const LAS bf16x8*)(kp), qf[0], acc, 0, 0, 0);
;                     acc = __builtin_amdgcn_mfma_f32_16x16x32_bf16(*(const LAS bf16x8*)(kp + 32), qf[1], acc, 0, 0, 0);
;                     const LAS float* rb = rpb + (r0 + c - gr + 7) * 31 + 15 - qcol;
; #pragma unroll
;                     for (int e = 0; e < 4; ++e) { const int kcol = kc0 + 16 * t2 + 4 * fq + e; const bool ok = (kcol >= cs) && (kcol < cs + 16);
;                         const float sv = ok ? acc[e] * 0.125f + rb[ok ? kcol : qcol] : -1.0e30f; acc[e] = sv; m = fmaxf(m, sv); }
;                     sl[2 * (c < 8 ? c : 0) + t2] = acc; }
	ds_read_b32 v240, v31 offset:37916
	ds_read_b32 v241, v31 offset:37920
	ds_read_b32 v242, v31 offset:37924
	ds_read_b32 v243, v31 offset:37928
	ds_read_b32 v244, v31 offset:37980
	ds_read_b32 v245, v31 offset:37984
	ds_read_b32 v246, v31 offset:37988
	ds_read_b32 v247, v31 offset:37992
	ds_read_b128 v[18:21], v32 offset:18432
	s_add_i32 s26, s26, s15
	s_add_i32 s0, s26, 0x10c0
	v_or_b32_e32 v24, s0, v88
	v_mov_b64_e32 v[22:23], s[8:9]
	s_lshl_b32 s1, s18, 7
	v_mad_i64_i32 v[22:23], s[18:19], v24, s72, v[22:23]
	v_lshlrev_b32_e32 v70, 1, v26
	v_lshl_add_u64 v[22:23], v[22:23], 0, v[70:71]
	s_lshl_b32 s2, s1, 1
	v_lshl_add_u64 v[22:23], v[22:23], 0, s[2:3]
	ds_read_b128 v[26:29], v32 offset:18496
	s_waitcnt lgkmcnt(1)
	v_mfma_f32_16x16x32_bf16 v[34:37], v[18:21], v[6:9], 0
	v_lshl_add_u64 v[248:249], v[22:23], 0, s[100:101]
	global_load_dwordx4 v[18:21], v[22:23], off offset:1024
	s_nop 0
	global_load_dwordx4 v[22:25], v[22:23], off offset:1152
	global_load_dword v250, v[248:249], off offset:1024
	global_load_dword v251, v[248:249], off offset:1152
	v_mov_b32_e32 v98, 0xf149f2ca
	v_mov_b32_e32 v100, 0xf149f2ca
	s_waitcnt lgkmcnt(0)
	v_mfma_f32_16x16x32_bf16 v[26:29], v[26:29], v[2:5], v[34:37]
	s_nop 2
	s_waitcnt lgkmcnt(0)
	s_nop 3
	v_fmac_f32_e32 v240, 0x3e000000, v26
	v_cndmask_b32_e64 v100, v100, v240, s[28:29]
	s_nop 2
	s_waitcnt lgkmcnt(0)
	s_nop 0
	v_fmac_f32_e32 v241, 0x3e000000, v27
	v_cndmask_b32_e64 v98, v98, v241, s[30:31]
	v_mov_b32_e32 v101, 0xf149f2ca
	v_mov_b32_e32 v102, 0xf149f2ca
	s_nop 2
	s_waitcnt lgkmcnt(0)
	v_fmac_f32_e32 v242, 0x3e000000, v28
	v_cndmask_b32_e64 v102, v102, v242, s[34:35]
	s_nop 2
	s_waitcnt lgkmcnt(0)
	v_fmac_f32_e32 v243, 0x3e000000, v29
	v_cndmask_b32_e64 v101, v101, v243, s[36:37]
	v_mul_u32_u24_e32 v26, 0x90, v33
	v_add_u32_e32 v33, v30, v26
	ds_read_b128 v[26:29], v33 offset:18432
	ds_read_b128 v[34:37], v33 offset:18496
	v_mov_b32_e32 v103, 0xf149f2ca
	v_mov_b32_e32 v105, 0xf149f2ca
	s_waitcnt lgkmcnt(1)
	v_mfma_f32_16x16x32_bf16 v[26:29], v[26:29], v[6:9], 0
	s_waitcnt lgkmcnt(0)
	v_mfma_f32_16x16x32_bf16 v[26:29], v[34:37], v[2:5], v[26:29]
	s_nop 2
	s_waitcnt lgkmcnt(0)
	s_nop 3
	v_fmac_f32_e32 v244, 0x3e000000, v26
	v_cndmask_b32_e64 v105, v105, v244, s[38:39]
	s_nop 2
	s_waitcnt lgkmcnt(0)
	s_nop 0
	v_fmac_f32_e32 v245, 0x3e000000, v27
	v_cndmask_b32_e64 v103, v103, v245, s[44:45]
	v_mov_b32_e32 v107, 0xf149f2ca
	v_mov_b32_e32 v109, 0xf149f2ca
	s_nop 2
	s_waitcnt lgkmcnt(0)
	v_fmac_f32_e32 v246, 0x3e000000, v28
	v_cndmask_b32_e64 v109, v109, v246, s[46:47]
	s_nop 2
	s_waitcnt lgkmcnt(0)
	v_fmac_f32_e32 v247, 0x3e000000, v29
	v_cndmask_b32_e64 v107, v107, v247, s[66:67]
	s_waitcnt vmcnt(7)
	ds_write_b128 v75, v[10:13]
	s_waitcnt vmcnt(6)
	ds_write_b128 v75, v[14:17] offset:9216
	s_waitcnt lgkmcnt(0)
	s_barrier
	ds_read_b32 v240, v31 offset:38040
	ds_read_b32 v241, v31 offset:38044
	ds_read_b32 v242, v31 offset:38048
	ds_read_b32 v243, v31 offset:38052
	ds_read_b32 v244, v31 offset:38104
	ds_read_b32 v245, v31 offset:38108
	ds_read_b32 v246, v31 offset:38112
	ds_read_b32 v247, v31 offset:38116
	ds_read_b128 v[10:13], v32
	ds_read_b128 v[26:29], v32 offset:64
	s_add_i32 s18, s26, 0x1100
	v_or_b32_e32 v16, s18, v88
	v_mov_b64_e32 v[14:15], s[8:9]
	v_mad_i64_i32 v[14:15], s[20:21], v16, s72, v[14:15]
	v_lshl_add_u64 v[14:15], v[14:15], 0, v[70:71]
	v_lshl_add_u64 v[14:15], v[14:15], 0, s[2:3]
	s_waitcnt lgkmcnt(1)
	v_mfma_f32_16x16x32_bf16 v[34:37], v[10:13], v[6:9], 0
	v_lshl_add_u64 v[248:249], v[14:15], 0, s[100:101]
	global_load_dwordx4 v[10:13], v[14:15], off offset:1024
	s_nop 0
	global_load_dwordx4 v[14:17], v[14:15], off offset:1152
	global_load_dword v250, v[248:249], off offset:1024
	global_load_dword v251, v[248:249], off offset:1152
	v_mov_b32_e32 v104, 0xf149f2ca
	v_mov_b32_e32 v106, 0xf149f2ca
	s_waitcnt lgkmcnt(0)
	v_mfma_f32_16x16x32_bf16 v[26:29], v[26:29], v[2:5], v[34:37]
	s_nop 2
	s_waitcnt lgkmcnt(0)
	s_nop 3
	v_fmac_f32_e32 v240, 0x3e000000, v26
	v_cndmask_b32_e64 v106, v106, v240, s[28:29]
	s_nop 2
	s_waitcnt lgkmcnt(0)
	s_nop 0
	v_fmac_f32_e32 v241, 0x3e000000, v27
	v_cndmask_b32_e64 v104, v104, v241, s[30:31]
	v_mov_b32_e32 v108, 0xf149f2ca
	v_mov_b32_e32 v110, 0xf149f2ca
	s_nop 2
	s_waitcnt lgkmcnt(0)
	v_fmac_f32_e32 v242, 0x3e000000, v28
	v_cndmask_b32_e64 v110, v110, v242, s[34:35]
	s_nop 2
	s_waitcnt lgkmcnt(0)
	v_fmac_f32_e32 v243, 0x3e000000, v29
	v_cndmask_b32_e64 v108, v108, v243, s[36:37]
	ds_read_b128 v[26:29], v33
	ds_read_b128 v[34:37], v33 offset:64
	v_mov_b32_e32 v111, 0xf149f2ca
	v_mov_b32_e32 v113, 0xf149f2ca
	s_waitcnt lgkmcnt(1)
	v_mfma_f32_16x16x32_bf16 v[26:29], v[26:29], v[6:9], 0
	s_waitcnt lgkmcnt(0)
	v_mfma_f32_16x16x32_bf16 v[26:29], v[34:37], v[2:5], v[26:29]
	s_nop 2
	s_waitcnt lgkmcnt(0)
	s_nop 3
	v_fmac_f32_e32 v244, 0x3e000000, v26
	v_cndmask_b32_e64 v113, v113, v244, s[38:39]
	s_nop 2
	s_waitcnt lgkmcnt(0)
	s_nop 0
	v_fmac_f32_e32 v245, 0x3e000000, v27
	v_cndmask_b32_e64 v111, v111, v245, s[44:45]
	v_mov_b32_e32 v112, 0xf149f2ca
	v_mov_b32_e32 v116, 0xf149f2ca
	s_nop 2
	s_waitcnt lgkmcnt(0)
	v_fmac_f32_e32 v246, 0x3e000000, v28
	v_cndmask_b32_e64 v116, v116, v246, s[46:47]
	s_nop 2
	s_waitcnt lgkmcnt(0)
	v_fmac_f32_e32 v247, 0x3e000000, v29
	v_cndmask_b32_e64 v112, v112, v247, s[66:67]
	s_waitcnt vmcnt(7)
	ds_write_b128 v75, v[18:21] offset:18432
	s_waitcnt vmcnt(6)
	ds_write_b128 v75, v[22:25] offset:27648
	s_waitcnt lgkmcnt(0)
	s_barrier
; #define LAS __attribute__((address_space(3)))
; template <bool LOCAL>
; __device__ __forceinline__ void na_unit(const bf16* P, const bf16* VT, bf16* YCAT, const LAS float* rpb_l, LAS bf16* buf, int b, int gr, int hp, int qblk, int tid) {
;     ...
;     for (int sidx = 0; sidx < 2 * NCH; ++sidx) {
;         if (sidx + 2 < 2 * NCH) NA_ISSUE(sidx + 2);
;         const LAS bf16* cb = buf + (sidx & 1) * 9216 + hh * 4608;
;         if (sidx < NCH) {
;             const int c = sidx;
;             if (LOCAL && c < 8) {
; #pragma unroll
;                 for (int t2 = 0; t2 < 2; ++t2) {
;                     const LAS bf16* kp = cb + (kc0 + 16 * t2 + fr) * 72 + 8 * fq;
;                     f32x4 acc = {0.f, 0.f, 0.f, 0.f};
;                     acc = __builtin_amdgcn_mfma_f32_16x16x32_bf16(*(const LAS bf16x8*)(kp), qf[0], acc, 0, 0, 0);
;                     acc = __builtin_amdgcn_mfma_f32_16x16x32_bf16(*(const LAS bf16x8*)(kp + 32), qf[1], acc, 0, 0, 0);
;                     const LAS float* rb = rpb + (r0 + c - gr + 7) * 31 + 15 - qcol;
; #pragma unroll
;                     for (int e = 0; e < 4; ++e) { const int kcol = kc0 + 16 * t2 + 4 * fq + e; const bool ok = (kcol >= cs) && (kcol < cs + 16);
;                         const float sv = ok ? acc[e] * 0.125f + rb[ok ? kcol : qcol] : -1.0e30f; acc[e] = sv; m = fmaxf(m, sv); }
;                     sl[2 * (c < 8 ? c : 0) + t2] = acc; }
	ds_read_b32 v240, v31 offset:38164
	ds_read_b32 v241, v31 offset:38168
	ds_read_b32 v242, v31 offset:38172
	ds_read_b32 v243, v31 offset:38176
	ds_read_b32 v244, v31 offset:38228
	ds_read_b32 v245, v31 offset:38232
	ds_read_b32 v246, v31 offset:38236
	ds_read_b32 v247, v31 offset:38240
	ds_read_b128 v[18:21], v32 offset:18432
	ds_read_b128 v[26:29], v32 offset:18496
	s_add_i32 s20, s26, 0x1140
	v_or_b32_e32 v24, s20, v88
	v_mov_b64_e32 v[22:23], s[8:9]
	v_mad_i64_i32 v[22:23], s[22:23], v24, s72, v[22:23]
	v_lshl_add_u64 v[22:23], v[22:23], 0, v[70:71]
	v_lshl_add_u64 v[22:23], v[22:23], 0, s[2:3]
	s_waitcnt lgkmcnt(1)
	v_mfma_f32_16x16x32_bf16 v[34:37], v[18:21], v[6:9], 0
	v_lshl_add_u64 v[248:249], v[22:23], 0, s[100:101]
	global_load_dwordx4 v[18:21], v[22:23], off offset:1024
	s_nop 0
	global_load_dwordx4 v[22:25], v[22:23], off offset:1152
	global_load_dword v250, v[248:249], off offset:1024
	global_load_dword v251, v[248:249], off offset:1152
	v_mov_b32_e32 v114, 0xf149f2ca
	v_mov_b32_e32 v115, 0xf149f2ca
	s_waitcnt lgkmcnt(0)
	v_mfma_f32_16x16x32_bf16 v[26:29], v[26:29], v[2:5], v[34:37]
	s_nop 2
	s_waitcnt lgkmcnt(0)
	s_nop 3
	v_fmac_f32_e32 v240, 0x3e000000, v26
	v_cndmask_b32_e64 v115, v115, v240, s[28:29]
	s_nop 2
	s_waitcnt lgkmcnt(0)
	s_nop 0
	v_fmac_f32_e32 v241, 0x3e000000, v27
	v_cndmask_b32_e64 v114, v114, v241, s[30:31]
	v_mov_b32_e32 v117, 0xf149f2ca
	v_mov_b32_e32 v118, 0xf149f2ca
	s_nop 2
	s_waitcnt lgkmcnt(0)
	v_fmac_f32_e32 v242, 0x3e000000, v28
	v_cndmask_b32_e64 v118, v118, v242, s[34:35]
	s_nop 2
	s_waitcnt lgkmcnt(0)
	v_fmac_f32_e32 v243, 0x3e000000, v29
	v_cndmask_b32_e64 v117, v117, v243, s[36:37]
	ds_read_b128 v[26:29], v33 offset:18432
	ds_read_b128 v[34:37], v33 offset:18496
	v_mov_b32_e32 v119, 0xf149f2ca
	v_mov_b32_e32 v121, 0xf149f2ca
	s_waitcnt lgkmcnt(1)
	v_mfma_f32_16x16x32_bf16 v[26:29], v[26:29], v[6:9], 0
	s_waitcnt lgkmcnt(0)
	v_mfma_f32_16x16x32_bf16 v[26:29], v[34:37], v[2:5], v[26:29]
	s_nop 2
	s_waitcnt lgkmcnt(0)
	s_nop 3
	v_fmac_f32_e32 v244, 0x3e000000, v26
	v_cndmask_b32_e64 v121, v121, v244, s[38:39]
	s_nop 2
	s_waitcnt lgkmcnt(0)
	s_nop 0
	v_fmac_f32_e32 v245, 0x3e000000, v27
	v_cndmask_b32_e64 v119, v119, v245, s[44:45]
	v_mov_b32_e32 v120, 0xf149f2ca
	v_mov_b32_e32 v124, 0xf149f2ca
	s_nop 2
	s_waitcnt lgkmcnt(0)
	v_fmac_f32_e32 v246, 0x3e000000, v28
	v_cndmask_b32_e64 v124, v124, v246, s[46:47]
	s_nop 2
	s_waitcnt lgkmcnt(0)
	v_fmac_f32_e32 v247, 0x3e000000, v29
	v_cndmask_b32_e64 v120, v120, v247, s[66:67]
	s_waitcnt vmcnt(7)
	ds_write_b128 v75, v[10:13]
	s_waitcnt vmcnt(6)
	ds_write_b128 v75, v[14:17] offset:9216
	s_waitcnt lgkmcnt(0)
	s_barrier
	ds_read_b32 v240, v31 offset:38288
	ds_read_b32 v241, v31 offset:38292
	ds_read_b32 v242, v31 offset:38296
	ds_read_b32 v243, v31 offset:38300
	ds_read_b32 v244, v31 offset:38352
	ds_read_b32 v245, v31 offset:38356
	ds_read_b32 v246, v31 offset:38360
	ds_read_b32 v247, v31 offset:38364
	ds_read_b128 v[10:13], v32
	ds_read_b128 v[26:29], v32 offset:64
	s_add_i32 s22, s26, 0x1180
	v_or_b32_e32 v16, s22, v88
	v_mov_b64_e32 v[14:15], s[8:9]
	v_mad_i64_i32 v[14:15], s[24:25], v16, s72, v[14:15]
	v_lshl_add_u64 v[14:15], v[14:15], 0, v[70:71]
	v_lshl_add_u64 v[14:15], v[14:15], 0, s[2:3]
	s_waitcnt lgkmcnt(1)
	v_mfma_f32_16x16x32_bf16 v[34:37], v[10:13], v[6:9], 0
	v_lshl_add_u64 v[248:249], v[14:15], 0, s[100:101]
	global_load_dwordx4 v[10:13], v[14:15], off offset:1024
	s_nop 0
	global_load_dwordx4 v[14:17], v[14:15], off offset:1152
	global_load_dword v250, v[248:249], off offset:1024
	global_load_dword v251, v[248:249], off offset:1152
	v_mov_b32_e32 v122, 0xf149f2ca
	v_mov_b32_e32 v123, 0xf149f2ca
	s_waitcnt lgkmcnt(0)
	v_mfma_f32_16x16x32_bf16 v[26:29], v[26:29], v[2:5], v[34:37]
	s_nop 2
	s_waitcnt lgkmcnt(0)
	s_nop 3
	v_fmac_f32_e32 v240, 0x3e000000, v26
	v_cndmask_b32_e64 v123, v123, v240, s[28:29]
	s_nop 2
	s_waitcnt lgkmcnt(0)
	s_nop 0
	v_fmac_f32_e32 v241, 0x3e000000, v27
	v_cndmask_b32_e64 v122, v122, v241, s[30:31]
	v_mov_b32_e32 v125, 0xf149f2ca
	v_mov_b32_e32 v126, 0xf149f2ca
	s_nop 2
	s_waitcnt lgkmcnt(0)
	v_fmac_f32_e32 v242, 0x3e000000, v28
	v_cndmask_b32_e64 v126, v126, v242, s[34:35]
	s_nop 2
	s_waitcnt lgkmcnt(0)
	v_fmac_f32_e32 v243, 0x3e000000, v29
	v_cndmask_b32_e64 v125, v125, v243, s[36:37]
	ds_read_b128 v[26:29], v33
	ds_read_b128 v[34:37], v33 offset:64
	v_mov_b32_e32 v127, 0xf149f2ca
	v_mov_b32_e32 v129, 0xf149f2ca
	s_waitcnt lgkmcnt(1)
	v_mfma_f32_16x16x32_bf16 v[26:29], v[26:29], v[6:9], 0
	s_waitcnt lgkmcnt(0)
	v_mfma_f32_16x16x32_bf16 v[26:29], v[34:37], v[2:5], v[26:29]
	s_nop 2
	s_waitcnt lgkmcnt(0)
	s_nop 3
	v_fmac_f32_e32 v244, 0x3e000000, v26
	v_cndmask_b32_e64 v129, v129, v244, s[38:39]
	s_nop 2
	s_waitcnt lgkmcnt(0)
	s_nop 0
	v_fmac_f32_e32 v245, 0x3e000000, v27
	v_cndmask_b32_e64 v127, v127, v245, s[44:45]
	v_mov_b32_e32 v128, 0xf149f2ca
	v_mov_b32_e32 v133, 0xf149f2ca
	s_nop 2
	s_waitcnt lgkmcnt(0)
	v_fmac_f32_e32 v246, 0x3e000000, v28
	v_cndmask_b32_e64 v133, v133, v246, s[46:47]
	s_nop 2
	s_waitcnt lgkmcnt(0)
	v_fmac_f32_e32 v247, 0x3e000000, v29
	v_cndmask_b32_e64 v128, v128, v247, s[66:67]
	s_waitcnt vmcnt(7)
	ds_write_b128 v75, v[18:21] offset:18432
	s_waitcnt vmcnt(6)
	ds_write_b128 v75, v[22:25] offset:27648
	s_waitcnt lgkmcnt(0)
	s_barrier
; #define LAS __attribute__((address_space(3)))
; template <bool LOCAL>
; __device__ __forceinline__ void na_unit(const bf16* P, const bf16* VT, bf16* YCAT, const LAS float* rpb_l, LAS bf16* buf, int b, int gr, int hp, int qblk, int tid) {
;     ...
;     for (int sidx = 0; sidx < 2 * NCH; ++sidx) {
;         if (sidx + 2 < 2 * NCH) NA_ISSUE(sidx + 2);
;         const LAS bf16* cb = buf + (sidx & 1) * 9216 + hh * 4608;
;         if (sidx < NCH) {
;             const int c = sidx;
;             if (LOCAL && c < 8) {
; #pragma unroll
;                 for (int t2 = 0; t2 < 2; ++t2) {
;                     const LAS bf16* kp = cb + (kc0 + 16 * t2 + fr) * 72 + 8 * fq;
;                     f32x4 acc = {0.f, 0.f, 0.f, 0.f};
;                     acc = __builtin_amdgcn_mfma_f32_16x16x32_bf16(*(const LAS bf16x8*)(kp), qf[0], acc, 0, 0, 0);
;                     acc = __builtin_amdgcn_mfma_f32_16x16x32_bf16(*(const LAS bf16x8*)(kp + 32), qf[1], acc, 0, 0, 0);
;                     const LAS float* rb = rpb + (r0 + c - gr + 7) * 31 + 15 - qcol;
; #pragma unroll
;                     for (int e = 0; e < 4; ++e) { const int kcol = kc0 + 16 * t2 + 4 * fq + e; const bool ok = (kcol >= cs) && (kcol < cs + 16);
;                         const float sv = ok ? acc[e] * 0.125f + rb[ok ? kcol : qcol] : -1.0e30f; acc[e] = sv; m = fmaxf(m, sv); }
;                     sl[2 * (c < 8 ? c : 0) + t2] = acc; }
	ds_read_b32 v240, v31 offset:38412
	ds_read_b32 v241, v31 offset:38416
	ds_read_b32 v242, v31 offset:38420
	ds_read_b32 v243, v31 offset:38424
	ds_read_b32 v244, v31 offset:38476
	ds_read_b32 v245, v31 offset:38480
	ds_read_b32 v246, v31 offset:38484
	ds_read_b32 v247, v31 offset:38488
	ds_read_b128 v[18:21], v32 offset:18432
	ds_read_b128 v[26:29], v32 offset:18496
	s_add_i32 s24, s26, 0x11c0
	v_or_b32_e32 v24, s24, v88
	v_mov_b64_e32 v[22:23], s[8:9]
	v_mad_i64_i32 v[22:23], s[26:27], v24, s72, v[22:23]
	v_lshl_add_u64 v[22:23], v[22:23], 0, v[70:71]
	v_lshl_add_u64 v[22:23], v[22:23], 0, s[2:3]
	s_waitcnt lgkmcnt(1)
	v_mfma_f32_16x16x32_bf16 v[34:37], v[18:21], v[6:9], 0
	global_load_dwordx4 v[18:21], v[22:23], off offset:1024
	s_nop 0
	global_load_dwordx4 v[22:25], v[22:23], off offset:1152
	v_mov_b32_e32 v130, 0xf149f2ca
	v_mov_b32_e32 v131, 0xf149f2ca
	s_waitcnt lgkmcnt(0)
	v_mfma_f32_16x16x32_bf16 v[26:29], v[26:29], v[2:5], v[34:37]
	s_nop 2
	s_waitcnt lgkmcnt(0)
	s_nop 3
	v_fmac_f32_e32 v240, 0x3e000000, v26
	v_cndmask_b32_e64 v131, v131, v240, s[28:29]
	s_nop 2
	s_waitcnt lgkmcnt(0)
	s_nop 0
	v_fmac_f32_e32 v241, 0x3e000000, v27
	v_cndmask_b32_e64 v130, v130, v241, s[30:31]
	v_mov_b32_e32 v134, 0xf149f2ca
	v_mov_b32_e32 v135, 0xf149f2ca
	s_nop 2
	s_waitcnt lgkmcnt(0)
	v_fmac_f32_e32 v242, 0x3e000000, v28
	v_cndmask_b32_e64 v135, v135, v242, s[34:35]
	s_nop 2
	s_waitcnt lgkmcnt(0)
	v_fmac_f32_e32 v243, 0x3e000000, v29
	v_cndmask_b32_e64 v134, v134, v243, s[36:37]
	ds_read_b128 v[26:29], v33 offset:18432
	ds_read_b128 v[34:37], v33 offset:18496
	v_mov_b32_e32 v137, 0xf149f2ca
	v_mov_b32_e32 v139, 0xf149f2ca
	s_waitcnt lgkmcnt(1)
	v_mfma_f32_16x16x32_bf16 v[26:29], v[26:29], v[6:9], 0
	s_waitcnt lgkmcnt(0)
	v_mfma_f32_16x16x32_bf16 v[26:29], v[34:37], v[2:5], v[26:29]
	s_nop 2
	s_waitcnt lgkmcnt(0)
	s_nop 3
	v_fmac_f32_e32 v244, 0x3e000000, v26
	v_cndmask_b32_e64 v139, v139, v244, s[38:39]
	s_nop 2
	s_waitcnt lgkmcnt(0)
	s_nop 0
	v_fmac_f32_e32 v245, 0x3e000000, v27
	v_cndmask_b32_e64 v137, v137, v245, s[44:45]
	v_mov_b32_e32 v138, 0xf149f2ca
	v_mov_b32_e32 v142, 0xf149f2ca
	s_nop 2
	s_waitcnt lgkmcnt(0)
	v_fmac_f32_e32 v246, 0x3e000000, v28
	v_cndmask_b32_e64 v142, v142, v246, s[46:47]
	s_nop 2
	s_waitcnt lgkmcnt(0)
	v_fmac_f32_e32 v247, 0x3e000000, v29
	v_cndmask_b32_e64 v138, v138, v247, s[66:67]
	s_waitcnt vmcnt(5)
	ds_write_b128 v75, v[10:13]
	s_waitcnt vmcnt(4)
	ds_write_b128 v75, v[14:17] offset:9216
	s_waitcnt lgkmcnt(0)
	s_barrier
	ds_read_b32 v240, v31 offset:38536
	ds_read_b32 v241, v31 offset:38540
	ds_read_b32 v242, v31 offset:38544
	ds_read_b32 v243, v31 offset:38548
	ds_read_b32 v244, v31 offset:38600
	ds_read_b32 v245, v31 offset:38604
	ds_read_b32 v246, v31 offset:38608
	ds_read_b32 v247, v31 offset:38612
	ds_read_b128 v[10:13], v32
	ds_read_b128 v[26:29], v32 offset:64
	s_lshl_b32 s26, s17, 8
	v_or_b32_e32 v34, s26, v88
	v_mov_b64_e32 v[14:15], s[8:9]
	v_mad_i64_i32 v[14:15], s[52:53], v34, s72, v[14:15]
	v_lshl_add_u64 v[14:15], v[14:15], 0, v[70:71]
	v_lshl_add_u64 v[14:15], v[14:15], 0, s[2:3]
	s_waitcnt lgkmcnt(1)
	v_mfma_f32_16x16x32_bf16 v[36:39], v[10:13], v[6:9], 0
	v_lshl_add_u64 v[248:249], v[14:15], 0, s[100:101]
	global_load_dwordx4 v[10:13], v[14:15], off offset:1024
	s_nop 0
	global_load_dwordx4 v[14:17], v[14:15], off offset:1152
	global_load_dword v250, v[248:249], off offset:1024
	global_load_dword v251, v[248:249], off offset:1152
	v_mov_b32_e32 v140, 0xf149f2ca
	v_mov_b32_e32 v141, 0xf149f2ca
	s_waitcnt lgkmcnt(0)
	v_mfma_f32_16x16x32_bf16 v[26:29], v[26:29], v[2:5], v[36:39]
	s_nop 2
	s_waitcnt lgkmcnt(0)
	s_nop 3
	v_fmac_f32_e32 v240, 0x3e000000, v26
	v_cndmask_b32_e64 v141, v141, v240, s[28:29]
	s_nop 2
	s_waitcnt lgkmcnt(0)
	s_nop 0
	v_fmac_f32_e32 v241, 0x3e000000, v27
	v_cndmask_b32_e64 v140, v140, v241, s[30:31]
	v_mov_b32_e32 v143, 0xf149f2ca
	v_mov_b32_e32 v144, 0xf149f2ca
	s_nop 2
	s_waitcnt lgkmcnt(0)
	v_fmac_f32_e32 v242, 0x3e000000, v28
	v_cndmask_b32_e64 v144, v144, v242, s[34:35]
	s_nop 2
	s_waitcnt lgkmcnt(0)
	v_fmac_f32_e32 v243, 0x3e000000, v29
	v_cndmask_b32_e64 v143, v143, v243, s[36:37]
	ds_read_b128 v[26:29], v33
	ds_read_b128 v[36:39], v33 offset:64
	v_mov_b32_e32 v145, 0xf149f2ca
	v_mov_b32_e32 v147, 0xf149f2ca
	s_waitcnt lgkmcnt(1)
	v_mfma_f32_16x16x32_bf16 v[26:29], v[26:29], v[6:9], 0
	s_waitcnt lgkmcnt(0)
	v_mfma_f32_16x16x32_bf16 v[26:29], v[36:39], v[2:5], v[26:29]
	s_nop 2
	s_waitcnt lgkmcnt(0)
	s_nop 3
	v_fmac_f32_e32 v244, 0x3e000000, v26
	v_cndmask_b32_e64 v147, v147, v244, s[38:39]
	s_nop 2
	s_waitcnt lgkmcnt(0)
	s_nop 0
	v_fmac_f32_e32 v245, 0x3e000000, v27
	v_cndmask_b32_e64 v145, v145, v245, s[44:45]
	v_mov_b32_e32 v146, 0xf149f2ca
	v_mov_b32_e32 v150, 0xf149f2ca
	s_nop 2
	s_waitcnt lgkmcnt(0)
	v_fmac_f32_e32 v246, 0x3e000000, v28
	v_cndmask_b32_e64 v150, v150, v246, s[46:47]
	s_nop 2
	s_waitcnt lgkmcnt(0)
	v_fmac_f32_e32 v247, 0x3e000000, v29
	v_cndmask_b32_e64 v146, v146, v247, s[66:67]
	s_waitcnt vmcnt(5)
	ds_write_b128 v75, v[18:21] offset:18432
	s_waitcnt vmcnt(4)
	ds_write_b128 v75, v[22:25] offset:27648
	s_waitcnt lgkmcnt(0)
	s_barrier
; #define LAS __attribute__((address_space(3)))
; template <bool LOCAL>
; __device__ __forceinline__ void na_unit(const bf16* P, const bf16* VT, bf16* YCAT, const LAS float* rpb_l, LAS bf16* buf, int b, int gr, int hp, int qblk, int tid) {
;     ...
;             if (LOCAL && c < 8) {
; #pragma unroll
;                 for (int t2 = 0; t2 < 2; ++t2) {
;                     const LAS bf16* kp = cb + (kc0 + 16 * t2 + fr) * 72 + 8 * fq;
;                     f32x4 acc = {0.f, 0.f, 0.f, 0.f};
;                     acc = __builtin_amdgcn_mfma_f32_16x16x32_bf16(*(const LAS bf16x8*)(kp), qf[0], acc, 0, 0, 0);
;                     acc = __builtin_amdgcn_mfma_f32_16x16x32_bf16(*(const LAS bf16x8*)(kp + 32), qf[1], acc, 0, 0, 0);
;                     const LAS float* rb = rpb + (r0 + c - gr + 7) * 31 + 15 - qcol;
; #pragma unroll
;                     for (int e = 0; e < 4; ++e) { const int kcol = kc0 + 16 * t2 + 4 * fq + e; const bool ok = (kcol >= cs) && (kcol < cs + 16);
;                         const float sv = ok ? acc[e] * 0.125f + rb[ok ? kcol : qcol] : -1.0e30f; acc[e] = sv; m = fmaxf(m, sv); }
;                     sl[2 * (c < 8 ? c : 0) + t2] = acc; }
;             } else {
;                 const int cc = c - NLOC;
; #pragma unroll
;                 for (int t4 = 0; t4 < 4; ++t4) {
;                     const LAS bf16* kp = cb + (16 * t4 + fr) * 72 + 8 * fq;
;                     f32x4 acc = {0.f, 0.f, 0.f, 0.f};
;                     acc = __builtin_amdgcn_mfma_f32_16x16x32_bf16(*(const LAS bf16x8*)(kp), qf[0], acc, 0, 0, 0);
;                     acc = __builtin_amdgcn_mfma_f32_16x16x32_bf16(*(const LAS bf16x8*)(kp + 32), qf[1], acc, 0, 0, 0);
; #pragma unroll
;                     for (int e = 0; e < 4; ++e) { acc[e] *= 0.125f; m = fmaxf(m, acc[e]); }
;                     sc[4 * (cc >= 0 ? cc : 0) + t4] = acc; }
;             }
;             if (sidx == NCH - 1) { m = fmaxf(m, __shfl_xor(m, 16)); m = fmaxf(m, __shfl_xor(m, 32)); }
	ds_read_b32 v240, v31 offset:38660
	ds_read_b32 v241, v31 offset:38664
	ds_read_b32 v242, v31 offset:38668
	ds_read_b32 v243, v31 offset:38672
	ds_read_b32 v244, v31 offset:38724
	ds_read_b32 v245, v31 offset:38728
	ds_read_b32 v246, v31 offset:38732
	ds_read_b32 v247, v31 offset:38736
	ds_read_b128 v[18:21], v32 offset:18432
	ds_read_b128 v[26:29], v32 offset:18496
	v_or_b32_e32 v24, 64, v34
	v_mov_b64_e32 v[22:23], s[8:9]
	v_mad_i64_i32 v[22:23], s[52:53], v24, s72, v[22:23]
	v_lshl_add_u64 v[22:23], v[22:23], 0, v[70:71]
	v_lshl_add_u64 v[22:23], v[22:23], 0, s[2:3]
	s_waitcnt lgkmcnt(1)
	v_mfma_f32_16x16x32_bf16 v[36:39], v[18:21], v[6:9], 0
	v_lshl_add_u64 v[248:249], v[22:23], 0, s[100:101]
	global_load_dwordx4 v[18:21], v[22:23], off offset:1024
	s_nop 0
	global_load_dwordx4 v[22:25], v[22:23], off offset:1152
	global_load_dword v250, v[248:249], off offset:1024
	global_load_dword v251, v[248:249], off offset:1152
	v_mov_b32_e32 v148, 0xf149f2ca
	v_mov_b32_e32 v149, 0xf149f2ca
	s_waitcnt lgkmcnt(0)
	v_mfma_f32_16x16x32_bf16 v[26:29], v[26:29], v[2:5], v[36:39]
	s_nop 2
	s_waitcnt lgkmcnt(0)
	s_nop 3
	v_fmac_f32_e32 v240, 0x3e000000, v26
	v_cndmask_b32_e64 v149, v149, v240, s[28:29]
	s_nop 2
	s_waitcnt lgkmcnt(0)
	s_nop 0
	v_fmac_f32_e32 v241, 0x3e000000, v27
	v_cndmask_b32_e64 v148, v148, v241, s[30:31]
	v_mov_b32_e32 v151, 0xf149f2ca
	v_mov_b32_e32 v152, 0xf149f2ca
	s_nop 2
	s_waitcnt lgkmcnt(0)
	v_fmac_f32_e32 v242, 0x3e000000, v28
	v_cndmask_b32_e64 v152, v152, v242, s[34:35]
	s_nop 2
	s_waitcnt lgkmcnt(0)
	v_fmac_f32_e32 v243, 0x3e000000, v29
	v_cndmask_b32_e64 v151, v151, v243, s[36:37]
	ds_read_b128 v[26:29], v33 offset:18432
	ds_read_b128 v[36:39], v33 offset:18496
	v_mov_b32_e32 v153, 0xf149f2ca
	v_mov_b32_e32 v155, 0xf149f2ca
	s_waitcnt lgkmcnt(1)
	v_mfma_f32_16x16x32_bf16 v[26:29], v[26:29], v[6:9], 0
	s_waitcnt lgkmcnt(0)
	v_mfma_f32_16x16x32_bf16 v[26:29], v[36:39], v[2:5], v[26:29]
	s_nop 2
	s_waitcnt lgkmcnt(0)
	s_nop 3
	v_fmac_f32_e32 v244, 0x3e000000, v26
	v_cndmask_b32_e64 v155, v155, v244, s[38:39]
	s_nop 2
	s_waitcnt lgkmcnt(0)
	s_nop 0
	v_fmac_f32_e32 v245, 0x3e000000, v27
	v_cndmask_b32_e64 v153, v153, v245, s[44:45]
	v_mov_b32_e32 v154, 0xf149f2ca
	v_mov_b32_e32 v157, 0xf149f2ca
	s_nop 2
	s_waitcnt lgkmcnt(0)
	v_fmac_f32_e32 v246, 0x3e000000, v28
	v_cndmask_b32_e64 v157, v157, v246, s[46:47]
	s_nop 2
	s_waitcnt lgkmcnt(0)
	v_fmac_f32_e32 v247, 0x3e000000, v29
	v_cndmask_b32_e64 v154, v154, v247, s[66:67]
	v_max3_f32 v26, v92, s75, v91
	v_max3_f32 v26, v26, v94, v93
	v_max3_f32 v26, v26, v96, v95
	v_max3_f32 v26, v26, v99, v97
	v_max3_f32 v26, v26, v100, v98
	v_max3_f32 v26, v26, v102, v101
	v_max3_f32 v26, v26, v105, v103
	v_max3_f32 v26, v26, v109, v107
	v_max3_f32 v26, v26, v106, v104
	v_max3_f32 v26, v26, v110, v108
	v_max3_f32 v26, v26, v113, v111
	v_max3_f32 v26, v26, v116, v112
	v_max3_f32 v26, v26, v115, v114
	v_max3_f32 v26, v26, v118, v117
	v_max3_f32 v26, v26, v121, v119
	v_max3_f32 v26, v26, v124, v120
	v_max3_f32 v26, v26, v123, v122
	v_max3_f32 v26, v26, v126, v125
	v_max3_f32 v26, v26, v129, v127
	v_max3_f32 v26, v26, v133, v128
	v_max3_f32 v26, v26, v131, v130
	v_max3_f32 v26, v26, v135, v134
	v_max3_f32 v26, v26, v139, v137
	v_max3_f32 v26, v26, v142, v138
	v_max3_f32 v26, v26, v141, v140
	v_max3_f32 v26, v26, v144, v143
	v_mad_u32_u24 v89, v89, s73, v30
	v_max3_f32 v26, v26, v147, v145
	s_waitcnt vmcnt(7)
	ds_write_b128 v75, v[10:13]
	s_waitcnt vmcnt(6)
	ds_write_b128 v75, v[14:17] offset:9216
	s_waitcnt lgkmcnt(0)
	s_barrier
	ds_read_b128 v[10:13], v89
	ds_read_b128 v[14:17], v89 offset:64
	v_max3_f32 v26, v26, v150, v146
	v_max3_f32 v26, v26, v149, v148
	v_max3_f32 v26, v26, v152, v151
	v_max3_f32 v26, v26, v155, v153
	v_max3_f32 v35, v26, v157, v154
	v_or_b32_e32 v26, 0x80, v34
	v_mov_b64_e32 v[44:45], s[8:9]
	v_mad_i64_i32 v[26:27], s[28:29], v26, s72, v[44:45]
	v_lshl_add_u64 v[26:27], v[26:27], 0, v[70:71]
	v_lshl_add_u64 v[30:31], v[26:27], 0, s[2:3]
	s_waitcnt lgkmcnt(1)
	v_mfma_f32_16x16x32_bf16 v[10:13], v[10:13], v[6:9], 0
	v_lshl_add_u64 v[248:249], v[30:31], 0, s[100:101]
	global_load_dwordx4 v[26:29], v[30:31], off offset:1024
	s_nop 0
	global_load_dwordx4 v[30:33], v[30:31], off offset:1152
	global_load_dword v250, v[248:249], off offset:1024
	global_load_dword v251, v[248:249], off offset:1152
	ds_read_b128 v[36:39], v89 offset:2304
	v_lshl_add_u64 v[78:79], s[4:5], 0, v[70:71]
	s_waitcnt lgkmcnt(1)
	v_mfma_f32_16x16x32_bf16 v[62:65], v[14:17], v[2:5], v[10:13]
	s_ashr_i32 s17, s16, 31
	v_mov_b32_e32 v81, v71
	v_cmp_lt_i32_e32 vcc, v83, v84
	ds_read_b128 v[10:13], v89 offset:2368
	v_add3_u32 v156, v86, v76, v87
	s_nop 2
	v_mul_f32_e32 v14, 0x3e000000, v62
	v_mul_f32_e32 v15, 0x3e000000, v63
	v_max3_f32 v35, v35, v14, v15
	v_mul_f32_e32 v40, 0x3e000000, v64
	s_waitcnt lgkmcnt(1)
	v_mfma_f32_16x16x32_bf16 v[14:17], v[36:39], v[6:9], 0
	v_mul_f32_e32 v36, 0x3e000000, v65
	v_max3_f32 v35, v35, v40, v36
	ds_read_b128 v[36:39], v89 offset:4608
	s_waitcnt lgkmcnt(1)
	v_mfma_f32_16x16x32_bf16 v[66:69], v[10:13], v[2:5], v[14:17]
	ds_read_b128 v[10:13], v89 offset:4672
	s_ashr_i32 s19, s18, 31
	s_ashr_i32 s21, s20, 31
	s_ashr_i32 s23, s22, 31
	s_ashr_i32 s25, s24, 31
	s_nop 2
	v_mul_f32_e32 v14, 0x3e000000, v66
	v_mul_f32_e32 v15, 0x3e000000, v67
	v_max3_f32 v35, v35, v14, v15
	s_waitcnt lgkmcnt(1)
	v_mfma_f32_16x16x32_bf16 v[14:17], v[36:39], v[6:9], 0
	v_mul_f32_e32 v40, 0x3e000000, v68
	v_mul_f32_e32 v41, 0x3e000000, v69
	v_max3_f32 v35, v35, v40, v41
	s_waitcnt lgkmcnt(0)
	v_mfma_f32_16x16x32_bf16 v[58:61], v[10:13], v[2:5], v[14:17]
	ds_read_b128 v[36:39], v89 offset:6912
	ds_read_b128 v[40:43], v89 offset:6976
	s_waitcnt vmcnt(7)
	ds_write_b128 v75, v[18:21] offset:18432
	s_waitcnt vmcnt(6)
	ds_write_b128 v75, v[22:25] offset:27648
	s_waitcnt lgkmcnt(0)
	s_nop 0
	v_mul_f32_e32 v10, 0x3e000000, v58
	v_mul_f32_e32 v11, 0x3e000000, v59
	v_max3_f32 v14, v35, v10, v11
	v_mfma_f32_16x16x32_bf16 v[10:13], v[36:39], v[6:9], 0
	v_mul_f32_e32 v15, 0x3e000000, v60
	v_mul_f32_e32 v16, 0x3e000000, v61
	v_max3_f32 v14, v14, v15, v16
	v_mfma_f32_16x16x32_bf16 v[54:57], v[40:43], v[2:5], v[10:13]
	s_barrier
; #define LAS __attribute__((address_space(3)))
; template <bool LOCAL>
; __device__ __forceinline__ void na_unit(const bf16* P, const bf16* VT, bf16* YCAT, const LAS float* rpb_l, LAS bf16* buf, int b, int gr, int hp, int qblk, int tid) {
;     ...
;                 const int cc = c - NLOC;
; #pragma unroll
;                 for (int t4 = 0; t4 < 4; ++t4) {
;                     const LAS bf16* kp = cb + (16 * t4 + fr) * 72 + 8 * fq;
;                     f32x4 acc = {0.f, 0.f, 0.f, 0.f};
;                     acc = __builtin_amdgcn_mfma_f32_16x16x32_bf16(*(const LAS bf16x8*)(kp), qf[0], acc, 0, 0, 0);
;                     acc = __builtin_amdgcn_mfma_f32_16x16x32_bf16(*(const LAS bf16x8*)(kp + 32), qf[1], acc, 0, 0, 0);
; #pragma unroll
;                     for (int e = 0; e < 4; ++e) { acc[e] *= 0.125f; m = fmaxf(m, acc[e]); }
;                     sc[4 * (cc >= 0 ? cc : 0) + t4] = acc; }
;             }
;             if (sidx == NCH - 1) { m = fmaxf(m, __shfl_xor(m, 16)); m = fmaxf(m, __shfl_xor(m, 32)); }
	v_or_b32_e32 v18, 0xc0, v34
	v_mad_i64_i32 v[18:19], s[28:29], v18, s72, v[44:45]
	v_lshl_add_u64 v[18:19], v[18:19], 0, v[70:71]
	s_nop 3
	v_mul_f32_e32 v10, 0x3e000000, v54
	v_mul_f32_e32 v11, 0x3e000000, v55
	v_max3_f32 v14, v14, v10, v11
	ds_read_b128 v[10:13], v89 offset:18432
	v_mul_f32_e32 v15, 0x3e000000, v56
	v_mul_f32_e32 v16, 0x3e000000, v57
	v_max3_f32 v35, v14, v15, v16
	ds_read_b128 v[14:17], v89 offset:18496
	v_lshl_add_u64 v[22:23], v[18:19], 0, s[2:3]
	s_waitcnt lgkmcnt(1)
	v_mfma_f32_16x16x32_bf16 v[10:13], v[10:13], v[6:9], 0
	global_load_dwordx4 v[18:21], v[22:23], off offset:1024
	global_load_dwordx4 v[158:161], v[22:23], off offset:1152
	ds_read_b128 v[22:25], v89 offset:20736
	s_ashr_i32 s27, s26, 31
	s_waitcnt lgkmcnt(1)
	v_mfma_f32_16x16x32_bf16 v[46:49], v[14:17], v[2:5], v[10:13]
	s_nop 2
	ds_read_b128 v[10:13], v89 offset:20800
	s_nop 3
	v_mul_f32_e32 v14, 0x3e000000, v46
	v_mul_f32_e32 v15, 0x3e000000, v47
	v_max3_f32 v34, v35, v14, v15
	v_mul_f32_e32 v35, 0x3e000000, v48
	s_waitcnt lgkmcnt(1)
	v_mfma_f32_16x16x32_bf16 v[14:17], v[22:25], v[6:9], 0
	v_mul_f32_e32 v22, 0x3e000000, v49
	v_max3_f32 v34, v34, v35, v22
	ds_read_b128 v[22:25], v89 offset:23040
	s_waitcnt lgkmcnt(1)
	v_mfma_f32_16x16x32_bf16 v[50:53], v[10:13], v[2:5], v[14:17]
	ds_read_b128 v[10:13], v89 offset:23104
	s_nop 6
	v_mul_f32_e32 v14, 0x3e000000, v50
	v_mul_f32_e32 v15, 0x3e000000, v51
	v_max3_f32 v34, v34, v14, v15
	s_waitcnt lgkmcnt(1)
	v_mfma_f32_16x16x32_bf16 v[14:17], v[22:25], v[6:9], 0
	v_mul_f32_e32 v35, 0x3e000000, v52
	v_mul_f32_e32 v36, 0x3e000000, v53
	v_max3_f32 v38, v34, v35, v36
	s_waitcnt lgkmcnt(0)
	v_mfma_f32_16x16x32_bf16 v[42:45], v[10:13], v[2:5], v[14:17]
	ds_read_b128 v[22:25], v89 offset:25344
	ds_read_b128 v[34:37], v89 offset:25408
	s_waitcnt vmcnt(5)
	ds_write_b128 v75, v[26:29]
	s_waitcnt vmcnt(4)
	ds_write_b128 v75, v[30:33] offset:9216
	s_waitcnt lgkmcnt(0)
	s_nop 0
	v_mul_f32_e32 v10, 0x3e000000, v42
	v_mul_f32_e32 v11, 0x3e000000, v43
	v_max3_f32 v14, v38, v10, v11
	v_mfma_f32_16x16x32_bf16 v[10:13], v[22:25], v[6:9], 0
	v_mul_f32_e32 v15, 0x3e000000, v44
	v_mul_f32_e32 v16, 0x3e000000, v45
	v_max3_f32 v14, v14, v15, v16
	v_mfma_f32_16x16x32_bf16 v[38:41], v[34:37], v[2:5], v[10:13]
	s_barrier
	v_add3_u32 v26, v88, s1, 64
	v_mul_u32_u24_e32 v26, 0x9000, v26
	v_lshl_add_u64 v[22:23], s[16:17], 1, v[78:79]
	s_nop 3
	v_mul_f32_e32 v10, 0x3e000000, v38
	v_mul_f32_e32 v11, 0x3e000000, v39
	v_max3_f32 v10, v14, v10, v11
	v_mul_f32_e32 v11, 0x3e000000, v40
	v_mul_f32_e32 v12, 0x3e000000, v41
	v_max3_f32 v34, v10, v11, v12
	v_or_b32_e32 v10, s1, v88
	v_mul_u32_u24_e32 v14, 0x9000, v10
	ds_read_b128 v[10:13], v89
	v_lshlrev_b32_e32 v70, 1, v14
	ds_read_b128 v[14:17], v89 offset:64
	v_lshlrev_b32_e32 v80, 1, v26
	v_lshl_add_u64 v[24:25], v[22:23], 0, v[70:71]
	v_lshl_add_u64 v[22:23], v[22:23], 0, v[80:81]
	s_waitcnt lgkmcnt(1)
	v_mfma_f32_16x16x32_bf16 v[10:13], v[10:13], v[6:9], 0
	v_lshl_add_u64 v[248:249], v[24:25], 0, 0
	v_lshl_add_u64 v[238:239], v[22:23], 0, 0
	global_load_dwordx4 v[162:165], v[24:25], off
	global_load_dwordx4 v[166:169], v[22:23], off
	global_load_dword v250, v[248:249], off offset:128
	global_load_dword v251, v[238:239], off offset:128
	ds_read_b128 v[22:25], v89 offset:2304
	s_add_i32 s16, s15, s50
	s_waitcnt lgkmcnt(1)
	v_mfma_f32_16x16x32_bf16 v[30:33], v[14:17], v[2:5], v[10:13]
	s_ashr_i32 s17, s16, 31
	s_ashr_i32 s15, s14, 31
	v_lshl_add_u64 v[86:87], s[14:15], 1, v[78:79]
	ds_read_b128 v[10:13], v89 offset:2368
	s_ashr_i32 s1, s0, 31
	s_nop 2
	v_mul_f32_e32 v14, 0x3e000000, v30
	v_mul_f32_e32 v15, 0x3e000000, v31
	v_max3_f32 v26, v34, v14, v15
	v_mul_f32_e32 v27, 0x3e000000, v32
	s_waitcnt lgkmcnt(1)
	v_mfma_f32_16x16x32_bf16 v[14:17], v[22:25], v[6:9], 0
	v_mul_f32_e32 v22, 0x3e000000, v33
	v_max3_f32 v26, v26, v27, v22
	ds_read_b128 v[22:25], v89 offset:4608
	s_waitcnt lgkmcnt(1)
	v_mfma_f32_16x16x32_bf16 v[34:37], v[10:13], v[2:5], v[14:17]
	ds_read_b128 v[10:13], v89 offset:4672
	s_nop 6
	v_mul_f32_e32 v14, 0x3e000000, v34
	v_mul_f32_e32 v15, 0x3e000000, v35
	v_max3_f32 v26, v26, v14, v15
	s_waitcnt lgkmcnt(1)
	v_mfma_f32_16x16x32_bf16 v[14:17], v[22:25], v[6:9], 0
	v_mul_f32_e32 v27, 0x3e000000, v36
	v_mul_f32_e32 v28, 0x3e000000, v37
	v_max3_f32 v88, v26, v27, v28
	s_waitcnt lgkmcnt(0)
	v_mfma_f32_16x16x32_bf16 v[26:29], v[10:13], v[2:5], v[14:17]
	ds_read_b128 v[22:25], v89 offset:6912
	ds_read_b128 v[172:175], v89 offset:6976
	s_waitcnt vmcnt(5)
	ds_write_b128 v75, v[18:21] offset:18432
	s_waitcnt vmcnt(4)
	ds_write_b128 v75, v[158:161] offset:27648
	s_waitcnt lgkmcnt(0)
	s_nop 0
	v_mul_f32_e32 v10, 0x3e000000, v26
	v_mul_f32_e32 v11, 0x3e000000, v27
	v_max3_f32 v14, v88, v10, v11
	v_mfma_f32_16x16x32_bf16 v[10:13], v[22:25], v[6:9], 0
	v_mul_f32_e32 v15, 0x3e000000, v28
	v_mul_f32_e32 v16, 0x3e000000, v29
	v_max3_f32 v14, v14, v15, v16
	v_mfma_f32_16x16x32_bf16 v[22:25], v[172:175], v[2:5], v[10:13]
	s_barrier
; #define LAS __attribute__((address_space(3)))
; __device__ __forceinline__ unsigned cvt_pk_bf16(float lo, float hi) { const float __attribute__((ext_vector_type(2))) v = {lo, hi}; return __builtin_bit_cast(unsigned, __builtin_convertvector(v, bf16x2_t)); }
; template <bool LOCAL>
; __device__ __forceinline__ void na_unit(const bf16* P, const bf16* VT, bf16* YCAT, const LAS float* rpb_l, LAS bf16* buf, int b, int gr, int hp, int qblk, int tid) {
;     ...
;             if (sidx == NCH - 1) { m = fmaxf(m, __shfl_xor(m, 16)); m = fmaxf(m, __shfl_xor(m, 32)); }
;         } else {
;             const int c = sidx - NCH;
;             if (LOCAL && c < 8) {
;                 float p[8];
; #pragma unroll
;                 for (int e = 0; e < 4; ++e) { p[e] = __expf(sl[2 * (c < 8 ? c : 0)][e] - m); p[4 + e] = __expf(sl[2 * (c < 8 ? c : 0) + 1][e] - m); }
; #pragma unroll
;                 for (int e = 0; e < 8; ++e) lsum += p[e];
;                 const bf16x8 pf = __builtin_bit_cast(bf16x8, (v4u){pg8::cvt_pk_bf16(p[0], p[1]), pg8::cvt_pk_bf16(p[2], p[3]), pg8::cvt_pk_bf16(p[4], p[5]), pg8::cvt_pk_bf16(p[6], p[7])});
; #pragma unroll
;                 for (int dt = 0; dt < 4; ++dt) { const LAS bf16* vp = cb + (16 * dt + fr) * 72 + kc0 + 4 * fq;
;                     o[dt] = __builtin_amdgcn_mfma_f32_16x16x32_bf16(frag44(vp, vp + 16), pf, o[dt], 0, 0, 0); }
	v_lshl_add_u64 v[18:19], s[16:17], 1, v[78:79]
	v_lshl_add_u64 v[20:21], v[18:19], 0, v[70:71]
	v_lshl_add_u64 v[18:19], v[18:19], 0, v[80:81]
	s_nop 3
	v_mul_f32_e32 v10, 0x3e000000, v22
	v_mul_f32_e32 v11, 0x3e000000, v23
	v_max3_f32 v14, v14, v10, v11
	ds_read_b128 v[10:13], v89 offset:18432
	v_mul_f32_e32 v15, 0x3e000000, v24
	v_mul_f32_e32 v16, 0x3e000000, v25
	v_max3_f32 v88, v14, v15, v16
	ds_read_b128 v[14:17], v89 offset:18496
	s_waitcnt lgkmcnt(1)
	v_mfma_f32_16x16x32_bf16 v[10:13], v[10:13], v[6:9], 0
	v_lshl_add_u64 v[248:249], v[20:21], 0, 0
	v_lshl_add_u64 v[238:239], v[18:19], 0, 0
	global_load_dwordx4 v[172:175], v[20:21], off
	global_load_dwordx4 v[176:179], v[18:19], off
	global_load_dword v250, v[248:249], off offset:128
	global_load_dword v251, v[238:239], off offset:128
	ds_read_b128 v[18:21], v89 offset:20736
	ds_read_b128 v[158:161], v89 offset:23040
	s_waitcnt lgkmcnt(2)
	v_mfma_f32_16x16x32_bf16 v[14:17], v[14:17], v[2:5], v[10:13]
	s_nop 2
	ds_read_b128 v[10:13], v89 offset:20800
	s_waitcnt lgkmcnt(2)
	v_mfma_f32_16x16x32_bf16 v[18:21], v[18:21], v[6:9], 0
	s_nop 1
	v_mul_f32_e32 v132, 0x3e000000, v14
	v_mul_f32_e32 v136, 0x3e000000, v15
	v_max3_f32 v88, v88, v132, v136
	s_waitcnt lgkmcnt(0)
	v_mfma_f32_16x16x32_bf16 v[18:21], v[10:13], v[2:5], v[18:21]
	ds_read_b128 v[10:13], v89 offset:23104
	ds_read_b128 v[180:183], v89 offset:25344
	ds_read_b128 v[184:187], v89 offset:25408
	v_mul_f32_e32 v132, 0x3e000000, v16
	v_mfma_f32_16x16x32_bf16 v[158:161], v[158:161], v[6:9], 0
	v_mul_f32_e32 v136, 0x3e000000, v17
	v_max3_f32 v88, v88, v132, v136
	s_nop 0
	v_mul_f32_e32 v132, 0x3e000000, v18
	s_waitcnt lgkmcnt(1)
	v_mfma_f32_16x16x32_bf16 v[6:9], v[180:183], v[6:9], 0
	v_mul_f32_e32 v136, 0x3e000000, v19
	v_max3_f32 v88, v88, v132, v136
	v_mul_f32_e32 v132, 0x3e000000, v20
	v_mfma_f32_16x16x32_bf16 v[10:13], v[10:13], v[2:5], v[158:161]
	v_mul_f32_e32 v136, 0x3e000000, v21
	v_max3_f32 v88, v88, v132, v136
	s_waitcnt vmcnt(7)
	ds_write_b128 v75, v[162:165]
	s_waitcnt vmcnt(6)
	ds_write_b128 v75, v[166:169] offset:9216
	s_waitcnt lgkmcnt(2)
	v_mfma_f32_16x16x32_bf16 v[2:5], v[184:187], v[2:5], v[6:9]
	v_mul_f32_e32 v89, 0x3e000000, v10
	v_mul_f32_e32 v132, 0x3e000000, v11
	v_max3_f32 v88, v88, v89, v132
	v_mul_f32_e32 v89, 0x3e000000, v12
	v_mul_f32_e32 v132, 0x3e000000, v13
	v_max3_f32 v88, v88, v89, v132
	s_nop 1
	v_mul_f32_e32 v6, 0x3e000000, v2
	v_mul_f32_e32 v7, 0x3e000000, v3
	v_max3_f32 v6, v88, v6, v7
	v_mul_f32_e32 v7, 0x3e000000, v4
	v_mul_f32_e32 v8, 0x3e000000, v5
	v_max3_f32 v6, v6, v7, v8
	v_cndmask_b32_e32 v7, v82, v83, vcc
	v_lshlrev_b32_e32 v88, 2, v7
	ds_bpermute_b32 v7, v88, v6
	v_cmp_lt_i32_e32 vcc, v85, v84
	v_lshl_add_u32 v8, v90, 1, v156
	s_waitcnt lgkmcnt(0)
	s_barrier
	v_max_f32_e32 v7, v7, v7
	v_max_f32_e32 v6, v6, v7
	v_cndmask_b32_e32 v7, v82, v85, vcc
	v_lshlrev_b32_e32 v89, 2, v7
	ds_bpermute_b32 v7, v89, v6
	s_waitcnt lgkmcnt(0)
	ds_read2_b64 v[158:161], v8 offset1:4
	v_max_f32_e32 v7, v7, v7
	v_max_f32_e32 v136, v6, v7
	v_sub_f32_e32 v6, v92, v136
	v_mul_f32_e32 v6, 0x3fb8aa3b, v6
	v_exp_f32_e32 v132, v6
	v_sub_f32_e32 v6, v96, v136
	v_mul_f32_e32 v6, 0x3fb8aa3b, v6
	v_exp_f32_e32 v92, v6
	v_sub_f32_e32 v6, v91, v136
	v_mul_f32_e32 v6, 0x3fb8aa3b, v6
	v_exp_f32_e32 v96, v6
	v_sub_f32_e32 v6, v95, v136
	v_mul_f32_e32 v6, 0x3fb8aa3b, v6
	v_exp_f32_e32 v91, v6
	v_sub_f32_e32 v6, v94, v136
	v_mul_f32_e32 v6, 0x3fb8aa3b, v6
	v_exp_f32_e32 v95, v6
	v_sub_f32_e32 v6, v99, v136
	v_mul_f32_e32 v6, 0x3fb8aa3b, v6
	v_exp_f32_e32 v94, v6
	v_sub_f32_e32 v6, v93, v136
	v_mul_f32_e32 v6, 0x3fb8aa3b, v6
	v_exp_f32_e32 v99, v6
	v_sub_f32_e32 v6, v97, v136
	v_mul_f32_e32 v6, 0x3fb8aa3b, v6
	v_exp_f32_e32 v93, v6
	v_cvt_pk_bf16_f32 v162, v132, v96
	v_cvt_pk_bf16_f32 v163, v95, v99
	v_cvt_pk_bf16_f32 v164, v92, v91
	v_cvt_pk_bf16_f32 v165, v94, v93
	v_add_u32_e32 v7, 0x800, v8
	v_add_u32_e32 v6, 0x1000, v8
	s_waitcnt lgkmcnt(0)
	v_mfma_f32_16x16x32_bf16 v[184:187], v[158:161], v[162:165], 0
	v_lshl_add_u64 v[158:159], v[86:87], 0, v[70:71]
	ds_read2_b64 v[166:169], v7 offset0:32 offset1:36
	ds_read2_b64 v[180:183], v6 offset0:64 offset1:68
	v_lshl_add_u64 v[86:87], v[86:87], 0, v[80:81]
	v_lshl_add_u64 v[248:249], v[158:159], 0, 0
	v_lshl_add_u64 v[238:239], v[86:87], 0, 0
	global_load_dwordx4 v[188:191], v[158:159], off
	global_load_dwordx4 v[192:195], v[86:87], off
	global_load_dword v250, v[248:249], off offset:128
	global_load_dword v251, v[238:239], off offset:128
	v_sub_f32_e32 v9, v100, v136
	v_mul_f32_e32 v9, 0x3fb8aa3b, v9
	v_add_u32_e32 v158, 0x1800, v8
	v_exp_f32_e32 v86, v9
	v_sub_f32_e32 v9, v105, v136
	ds_read2_b64 v[196:199], v158 offset0:96 offset1:100
	v_mul_f32_e32 v9, 0x3fb8aa3b, v9
	v_exp_f32_e32 v76, v9
	v_sub_f32_e32 v9, v98, v136
	v_mul_f32_e32 v9, 0x3fb8aa3b, v9
	v_exp_f32_e32 v90, v9
	v_sub_f32_e32 v9, v103, v136
	v_mul_f32_e32 v9, 0x3fb8aa3b, v9
	v_exp_f32_e32 v87, v9
	v_sub_f32_e32 v9, v102, v136
	v_mul_f32_e32 v9, 0x3fb8aa3b, v9
	v_exp_f32_e32 v98, v9
	v_sub_f32_e32 v9, v109, v136
	v_mul_f32_e32 v9, 0x3fb8aa3b, v9
	v_add_u32_e32 v160, 0x4800, v8
	s_waitcnt lgkmcnt(2)
	v_mfma_f32_16x16x32_bf16 v[166:169], v[166:169], v[162:165], 0
	s_waitcnt vmcnt(7)
	ds_write_b128 v75, v[172:175] offset:18432
	s_waitcnt vmcnt(6)
	ds_write_b128 v75, v[176:179] offset:27648
	s_waitcnt lgkmcnt(0)
	s_barrier
; #define LAS __attribute__((address_space(3)))
; __device__ __forceinline__ unsigned cvt_pk_bf16(float lo, float hi) { const float __attribute__((ext_vector_type(2))) v = {lo, hi}; return __builtin_bit_cast(unsigned, __builtin_convertvector(v, bf16x2_t)); }
; template <bool LOCAL>
; __device__ __forceinline__ void na_unit(const bf16* P, const bf16* VT, bf16* YCAT, const LAS float* rpb_l, LAS bf16* buf, int b, int gr, int hp, int qblk, int tid) {
;     ...
;             const int c = sidx - NCH;
;             if (LOCAL && c < 8) {
;                 float p[8];
; #pragma unroll
;                 for (int e = 0; e < 4; ++e) { p[e] = __expf(sl[2 * (c < 8 ? c : 0)][e] - m); p[4 + e] = __expf(sl[2 * (c < 8 ? c : 0) + 1][e] - m); }
; #pragma unroll
;                 for (int e = 0; e < 8; ++e) lsum += p[e];
;                 const bf16x8 pf = __builtin_bit_cast(bf16x8, (v4u){pg8::cvt_pk_bf16(p[0], p[1]), pg8::cvt_pk_bf16(p[2], p[3]), pg8::cvt_pk_bf16(p[4], p[5]), pg8::cvt_pk_bf16(p[6], p[7])});
; #pragma unroll
;                 for (int dt = 0; dt < 4; ++dt) { const LAS bf16* vp = cb + (16 * dt + fr) * 72 + kc0 + 4 * fq;
;                     o[dt] = __builtin_amdgcn_mfma_f32_16x16x32_bf16(frag44(vp, vp + 16), pf, o[dt], 0, 0, 0); }
;             } else {
;                 const int cc = c - NLOC;
; #pragma unroll
;                 for (int p2 = 0; p2 < 2; ++p2) {
;                     float p[8];
; #pragma unroll
;                     for (int e = 0; e < 4; ++e) { p[e] = __expf(sc[4 * (cc >= 0 ? cc : 0) + 2 * p2][e] - m); p[4 + e] = __expf(sc[4 * (cc >= 0 ? cc : 0) + 2 * p2 + 1][e] - m); }
; #pragma unroll
;                     for (int e = 0; e < 8; ++e) lsum += p[e];
;                     const bf16x8 pf = __builtin_bit_cast(bf16x8, (v4u){pg8::cvt_pk_bf16(p[0], p[1]), pg8::cvt_pk_bf16(p[2], p[3]), pg8::cvt_pk_bf16(p[4], p[5]), pg8::cvt_pk_bf16(p[6], p[7])});
; #pragma unroll
;                     for (int dt = 0; dt < 4; ++dt) { const LAS bf16* vp = cb + (16 * dt + fr) * 72 + 32 * p2 + 4 * fq;
;                         o[dt] = __builtin_amdgcn_mfma_f32_16x16x32_bf16(frag44(vp, vp + 16), pf, o[dt], 0, 0, 0); }
;                 }
;             }
;         }
;         if (sidx + 1 < 2 * NCH) NA_STORE(sidx + 1);
	v_mfma_f32_16x16x32_bf16 v[180:183], v[180:183], v[162:165], 0
	v_exp_f32_e32 v97, v9
	v_sub_f32_e32 v9, v101, v136
	v_mfma_f32_16x16x32_bf16 v[196:199], v[196:199], v[162:165], 0
	ds_read2_b64 v[162:165], v160 offset1:4
	v_add_u32_e32 v159, 0x5000, v8
	v_mul_f32_e32 v9, 0x3fb8aa3b, v9
	ds_read2_b64 v[172:175], v159 offset0:32 offset1:36
	v_exp_f32_e32 v100, v9
	v_sub_f32_e32 v9, v107, v136
	v_mul_f32_e32 v9, 0x3fb8aa3b, v9
	v_exp_f32_e32 v101, v9
	v_cvt_pk_bf16_f32 v176, v86, v90
	v_cvt_pk_bf16_f32 v177, v98, v100
	v_cvt_pk_bf16_f32 v178, v76, v87
	v_cvt_pk_bf16_f32 v179, v97, v101
	v_lshl_add_u64 v[102:103], s[0:1], 1, v[78:79]
	v_add_u32_e32 v161, 0x5800, v8
	s_waitcnt lgkmcnt(1)
	v_mfma_f32_16x16x32_bf16 v[184:187], v[162:165], v[176:179], v[184:187]
	v_lshl_add_u64 v[162:163], v[102:103], 0, v[70:71]
	v_lshl_add_u64 v[102:103], v[102:103], 0, v[80:81]
	v_sub_f32_e32 v9, v106, v136
	s_waitcnt lgkmcnt(0)
	v_mfma_f32_16x16x32_bf16 v[164:167], v[172:175], v[176:179], v[166:169]
	ds_read2_b64 v[172:175], v161 offset0:64 offset1:68
	v_lshl_add_u64 v[248:249], v[162:163], 0, 0
	v_lshl_add_u64 v[238:239], v[102:103], 0, 0
	global_load_dwordx4 v[200:203], v[162:163], off
	global_load_dwordx4 v[204:207], v[102:103], off
	global_load_dword v250, v[248:249], off offset:128
	global_load_dword v251, v[238:239], off offset:128
	v_mul_f32_e32 v9, 0x3fb8aa3b, v9
	v_add_u32_e32 v162, 0x6000, v8
	v_exp_f32_e32 v103, v9
	v_sub_f32_e32 v9, v113, v136
	s_waitcnt lgkmcnt(0)
	v_mfma_f32_16x16x32_bf16 v[172:175], v[172:175], v[176:179], v[180:183]
	s_nop 2
	ds_read2_b64 v[180:183], v162 offset0:96 offset1:100
	v_mul_f32_e32 v9, 0x3fb8aa3b, v9
	v_exp_f32_e32 v102, v9
	v_sub_f32_e32 v9, v104, v136
	v_mul_f32_e32 v9, 0x3fb8aa3b, v9
	v_exp_f32_e32 v105, v9
	v_sub_f32_e32 v9, v111, v136
	v_mul_f32_e32 v9, 0x3fb8aa3b, v9
	v_exp_f32_e32 v104, v9
	v_sub_f32_e32 v9, v110, v136
	v_mul_f32_e32 v9, 0x3fb8aa3b, v9
	v_exp_f32_e32 v107, v9
	v_sub_f32_e32 v9, v116, v136
	v_mul_f32_e32 v9, 0x3fb8aa3b, v9
	s_waitcnt lgkmcnt(0)
	v_mfma_f32_16x16x32_bf16 v[176:179], v[180:183], v[176:179], v[196:199]
	s_waitcnt vmcnt(7)
	ds_write_b128 v75, v[188:191]
	s_waitcnt vmcnt(6)
	ds_write_b128 v75, v[192:195] offset:9216
	s_waitcnt lgkmcnt(0)
	s_barrier
	v_exp_f32_e32 v106, v9
	v_sub_f32_e32 v9, v108, v136
	ds_read2_b64 v[180:183], v8 offset1:4
	v_mul_f32_e32 v9, 0x3fb8aa3b, v9
	v_exp_f32_e32 v108, v9
	v_sub_f32_e32 v9, v112, v136
	v_mul_f32_e32 v9, 0x3fb8aa3b, v9
	v_exp_f32_e32 v109, v9
	v_lshl_add_u64 v[168:169], s[18:19], 1, v[78:79]
	v_cvt_pk_bf16_f32 v188, v103, v105
	v_cvt_pk_bf16_f32 v189, v107, v108
	v_cvt_pk_bf16_f32 v190, v102, v104
	v_cvt_pk_bf16_f32 v191, v106, v109
	v_lshl_add_u64 v[192:193], v[168:169], 0, v[70:71]
	ds_read2_b64 v[110:113], v7 offset0:32 offset1:36
	s_waitcnt lgkmcnt(1)
	v_mfma_f32_16x16x32_bf16 v[180:183], v[180:183], v[188:191], v[184:187]
	v_lshl_add_u64 v[168:169], v[168:169], 0, v[80:81]
	v_sub_f32_e32 v9, v115, v136
	v_mul_f32_e32 v9, 0x3fb8aa3b, v9
	ds_read2_b64 v[184:187], v6 offset0:64 offset1:68
	v_lshl_add_u64 v[248:249], v[192:193], 0, 0
	v_lshl_add_u64 v[238:239], v[168:169], 0, 0
	global_load_dwordx4 v[192:195], v[192:193], off
	s_nop 0
	global_load_dwordx4 v[196:199], v[168:169], off
	global_load_dword v250, v[248:249], off offset:128
	global_load_dword v251, v[238:239], off offset:128
	s_waitcnt lgkmcnt(1)
	v_mfma_f32_16x16x32_bf16 v[164:167], v[110:113], v[188:191], v[164:167]
	ds_read2_b64 v[110:113], v158 offset0:96 offset1:100
	s_waitcnt vmcnt(7)
	ds_write_b128 v75, v[200:203] offset:18432
	s_waitcnt vmcnt(6)
	ds_write_b128 v75, v[204:207] offset:27648
	s_waitcnt lgkmcnt(2)
	v_mfma_f32_16x16x32_bf16 v[176:179], v[110:113], v[188:191], v[176:179]
	v_exp_f32_e32 v111, v9
	v_sub_f32_e32 v9, v121, v136
	v_mul_f32_e32 v9, 0x3fb8aa3b, v9
	v_exp_f32_e32 v110, v9
	v_sub_f32_e32 v9, v114, v136
	v_mul_f32_e32 v9, 0x3fb8aa3b, v9
	v_exp_f32_e32 v113, v9
	v_sub_f32_e32 v9, v119, v136
	v_mul_f32_e32 v9, 0x3fb8aa3b, v9
	v_exp_f32_e32 v112, v9
	v_sub_f32_e32 v9, v118, v136
	v_mul_f32_e32 v9, 0x3fb8aa3b, v9
	v_exp_f32_e32 v115, v9
	v_sub_f32_e32 v9, v124, v136
	v_mul_f32_e32 v9, 0x3fb8aa3b, v9
	v_exp_f32_e32 v114, v9
	v_sub_f32_e32 v9, v117, v136
	v_mul_f32_e32 v9, 0x3fb8aa3b, v9
	v_mfma_f32_16x16x32_bf16 v[172:175], v[184:187], v[188:191], v[172:175]
	s_waitcnt lgkmcnt(0)
	s_barrier
	v_exp_f32_e32 v116, v9
	ds_read2_b64 v[184:187], v160 offset1:4
	v_sub_f32_e32 v9, v120, v136
	ds_read2_b64 v[118:121], v159 offset0:32 offset1:36
	v_mul_f32_e32 v9, 0x3fb8aa3b, v9
	v_exp_f32_e32 v117, v9
	v_lshl_add_u64 v[168:169], s[20:21], 1, v[78:79]
	v_lshl_add_u64 v[200:201], v[168:169], 0, v[70:71]
	v_cvt_pk_bf16_f32 v188, v111, v113
	v_cvt_pk_bf16_f32 v189, v115, v116
	v_cvt_pk_bf16_f32 v190, v110, v112
	v_cvt_pk_bf16_f32 v191, v114, v117
	v_lshl_add_u64 v[168:169], v[168:169], 0, v[80:81]
	v_sub_f32_e32 v9, v123, v136
	s_waitcnt lgkmcnt(1)
	v_mfma_f32_16x16x32_bf16 v[180:183], v[184:187], v[188:191], v[180:183]
	v_lshl_add_u64 v[248:249], v[200:201], 0, 0
	v_lshl_add_u64 v[238:239], v[168:169], 0, 0
	global_load_dwordx4 v[184:187], v[200:201], off
	s_nop 0
	global_load_dwordx4 v[200:203], v[168:169], off
	global_load_dword v250, v[248:249], off offset:128
	global_load_dword v251, v[238:239], off offset:128
	v_mul_f32_e32 v9, 0x3fb8aa3b, v9
	v_lshl_add_u64 v[168:169], s[22:23], 1, v[78:79]
	s_waitcnt lgkmcnt(0)
	v_mfma_f32_16x16x32_bf16 v[164:167], v[118:121], v[188:191], v[164:167]
	ds_read2_b64 v[118:121], v161 offset0:64 offset1:68
	v_fma_f32 v62, v62, s74, -v136
	v_fma_f32 v63, v63, s74, -v136
	s_waitcnt lgkmcnt(0)
	v_mfma_f32_16x16x32_bf16 v[172:175], v[118:121], v[188:191], v[172:175]
	ds_read2_b64 v[118:121], v162 offset0:96 offset1:100
	s_waitcnt vmcnt(7)
	ds_write_b128 v75, v[192:195]
	s_waitcnt vmcnt(6)
	ds_write_b128 v75, v[196:199] offset:9216
	s_waitcnt lgkmcnt(0)
	v_mfma_f32_16x16x32_bf16 v[176:179], v[118:121], v[188:191], v[176:179]
	v_exp_f32_e32 v119, v9
	v_sub_f32_e32 v9, v129, v136
	v_mul_f32_e32 v9, 0x3fb8aa3b, v9
	v_exp_f32_e32 v118, v9
	v_sub_f32_e32 v9, v122, v136
	v_mul_f32_e32 v9, 0x3fb8aa3b, v9
	v_exp_f32_e32 v121, v9
	v_sub_f32_e32 v9, v127, v136
	v_mul_f32_e32 v9, 0x3fb8aa3b, v9
	v_exp_f32_e32 v120, v9
	v_sub_f32_e32 v9, v126, v136
	v_mul_f32_e32 v9, 0x3fb8aa3b, v9
	v_exp_f32_e32 v123, v9
	v_sub_f32_e32 v9, v133, v136
	v_mul_f32_e32 v9, 0x3fb8aa3b, v9
	s_barrier
; #define LAS __attribute__((address_space(3)))
; __device__ __forceinline__ unsigned cvt_pk_bf16(float lo, float hi) { const float __attribute__((ext_vector_type(2))) v = {lo, hi}; return __builtin_bit_cast(unsigned, __builtin_convertvector(v, bf16x2_t)); }
; template <bool LOCAL>
; __device__ __forceinline__ void na_unit(const bf16* P, const bf16* VT, bf16* YCAT, const LAS float* rpb_l, LAS bf16* buf, int b, int gr, int hp, int qblk, int tid) {
;     ...
;             const int c = sidx - NCH;
;             if (LOCAL && c < 8) {
;                 float p[8];
; #pragma unroll
;                 for (int e = 0; e < 4; ++e) { p[e] = __expf(sl[2 * (c < 8 ? c : 0)][e] - m); p[4 + e] = __expf(sl[2 * (c < 8 ? c : 0) + 1][e] - m); }
; #pragma unroll
;                 for (int e = 0; e < 8; ++e) lsum += p[e];
;                 const bf16x8 pf = __builtin_bit_cast(bf16x8, (v4u){pg8::cvt_pk_bf16(p[0], p[1]), pg8::cvt_pk_bf16(p[2], p[3]), pg8::cvt_pk_bf16(p[4], p[5]), pg8::cvt_pk_bf16(p[6], p[7])});
; #pragma unroll
;                 for (int dt = 0; dt < 4; ++dt) { const LAS bf16* vp = cb + (16 * dt + fr) * 72 + kc0 + 4 * fq;
;                     o[dt] = __builtin_amdgcn_mfma_f32_16x16x32_bf16(frag44(vp, vp + 16), pf, o[dt], 0, 0, 0); }
;             } else {
;                 const int cc = c - NLOC;
; #pragma unroll
;                 for (int p2 = 0; p2 < 2; ++p2) {
;                     float p[8];
; #pragma unroll
;                     for (int e = 0; e < 4; ++e) { p[e] = __expf(sc[4 * (cc >= 0 ? cc : 0) + 2 * p2][e] - m); p[4 + e] = __expf(sc[4 * (cc >= 0 ? cc : 0) + 2 * p2 + 1][e] - m); }
; #pragma unroll
;                     for (int e = 0; e < 8; ++e) lsum += p[e];
;                     const bf16x8 pf = __builtin_bit_cast(bf16x8, (v4u){pg8::cvt_pk_bf16(p[0], p[1]), pg8::cvt_pk_bf16(p[2], p[3]), pg8::cvt_pk_bf16(p[4], p[5]), pg8::cvt_pk_bf16(p[6], p[7])});
; #pragma unroll
;                     for (int dt = 0; dt < 4; ++dt) { const LAS bf16* vp = cb + (16 * dt + fr) * 72 + 32 * p2 + 4 * fq;
;                         o[dt] = __builtin_amdgcn_mfma_f32_16x16x32_bf16(frag44(vp, vp + 16), pf, o[dt], 0, 0, 0); }
;                 }
;             }
;         }
;         if (sidx + 1 < 2 * NCH) NA_STORE(sidx + 1);
	v_exp_f32_e32 v122, v9
	v_sub_f32_e32 v9, v125, v136
	ds_read2_b64 v[188:191], v8 offset1:4
	v_mul_f32_e32 v9, 0x3fb8aa3b, v9
	v_exp_f32_e32 v124, v9
	v_sub_f32_e32 v9, v128, v136
	v_mul_f32_e32 v9, 0x3fb8aa3b, v9
	v_exp_f32_e32 v125, v9
	v_cvt_pk_bf16_f32 v192, v119, v121
	v_cvt_pk_bf16_f32 v193, v123, v124
	v_cvt_pk_bf16_f32 v194, v118, v120
	v_cvt_pk_bf16_f32 v195, v122, v125
	v_lshl_add_u64 v[196:197], v[168:169], 0, v[70:71]
	ds_read2_b64 v[126:129], v7 offset0:32 offset1:36
	s_waitcnt lgkmcnt(1)
	v_mfma_f32_16x16x32_bf16 v[180:183], v[188:191], v[192:195], v[180:183]
	ds_read2_b64 v[188:191], v6 offset0:64 offset1:68
	v_lshl_add_u64 v[168:169], v[168:169], 0, v[80:81]
	v_lshl_add_u64 v[248:249], v[196:197], 0, 0
	v_lshl_add_u64 v[238:239], v[168:169], 0, 0
	global_load_dwordx4 v[196:199], v[196:197], off
	s_nop 0
	global_load_dwordx4 v[204:207], v[168:169], off
	global_load_dword v250, v[248:249], off offset:128
	global_load_dword v251, v[238:239], off offset:128
	s_waitcnt lgkmcnt(1)
	v_mfma_f32_16x16x32_bf16 v[164:167], v[126:129], v[192:195], v[164:167]
	ds_read2_b64 v[126:129], v158 offset0:96 offset1:100
	v_sub_f32_e32 v9, v131, v136
	v_mul_f32_e32 v9, 0x3fb8aa3b, v9
	s_waitcnt lgkmcnt(0)
	v_mfma_f32_16x16x32_bf16 v[176:179], v[126:129], v[192:195], v[176:179]
	v_exp_f32_e32 v127, v9
	v_sub_f32_e32 v9, v139, v136
	v_mul_f32_e32 v9, 0x3fb8aa3b, v9
	v_exp_f32_e32 v126, v9
	v_sub_f32_e32 v9, v130, v136
	v_mul_f32_e32 v9, 0x3fb8aa3b, v9
	v_exp_f32_e32 v129, v9
	v_sub_f32_e32 v9, v137, v136
	v_mul_f32_e32 v9, 0x3fb8aa3b, v9
	v_exp_f32_e32 v128, v9
	v_sub_f32_e32 v9, v135, v136
	v_mul_f32_e32 v9, 0x3fb8aa3b, v9
	v_exp_f32_e32 v131, v9
	v_sub_f32_e32 v9, v142, v136
	v_mul_f32_e32 v9, 0x3fb8aa3b, v9
	v_mfma_f32_16x16x32_bf16 v[172:175], v[188:191], v[192:195], v[172:175]
	s_waitcnt vmcnt(7)
	ds_write_b128 v75, v[184:187] offset:18432
	s_waitcnt vmcnt(6)
	ds_write_b128 v75, v[200:203] offset:27648
	s_waitcnt lgkmcnt(0)
	s_barrier
	v_exp_f32_e32 v130, v9
	v_sub_f32_e32 v9, v134, v136
	ds_read2_b64 v[184:187], v160 offset1:4
	ds_read2_b64 v[188:191], v159 offset0:32 offset1:36
	v_mul_f32_e32 v9, 0x3fb8aa3b, v9
	v_exp_f32_e32 v133, v9
	v_sub_f32_e32 v9, v138, v136
	v_mul_f32_e32 v9, 0x3fb8aa3b, v9
	v_exp_f32_e32 v134, v9
	v_lshl_add_u64 v[168:169], s[24:25], 1, v[78:79]
	v_lshl_add_u64 v[200:201], v[168:169], 0, v[70:71]
	v_cvt_pk_bf16_f32 v192, v127, v129
	v_cvt_pk_bf16_f32 v193, v131, v133
	v_cvt_pk_bf16_f32 v194, v126, v128
	v_cvt_pk_bf16_f32 v195, v130, v134
	v_lshl_add_u64 v[138:139], v[168:169], 0, v[80:81]
	v_sub_f32_e32 v9, v141, v136
	s_waitcnt lgkmcnt(1)
	v_mfma_f32_16x16x32_bf16 v[180:183], v[184:187], v[192:195], v[180:183]
	global_load_dwordx4 v[184:187], v[200:201], off
	s_nop 0
	global_load_dwordx4 v[200:203], v[138:139], off
	v_mul_f32_e32 v9, 0x3fb8aa3b, v9
	v_exp_f32_e32 v137, v9
	s_waitcnt lgkmcnt(0)
	v_mfma_f32_16x16x32_bf16 v[164:167], v[188:191], v[192:195], v[164:167]
	ds_read2_b64 v[188:191], v161 offset0:64 offset1:68
	v_sub_f32_e32 v9, v147, v136
	v_mul_f32_e32 v9, 0x3fb8aa3b, v9
	s_waitcnt lgkmcnt(0)
	v_mfma_f32_16x16x32_bf16 v[172:175], v[188:191], v[192:195], v[172:175]
	ds_read2_b64 v[188:191], v162 offset0:96 offset1:100
	v_exp_f32_e32 v135, v9
	v_sub_f32_e32 v9, v140, v136
	v_mul_f32_e32 v9, 0x3fb8aa3b, v9
	v_exp_f32_e32 v139, v9
	v_sub_f32_e32 v9, v145, v136
	v_mul_f32_e32 v9, 0x3fb8aa3b, v9
	v_exp_f32_e32 v138, v9
	v_sub_f32_e32 v9, v144, v136
	v_mul_f32_e32 v9, 0x3fb8aa3b, v9
	s_waitcnt lgkmcnt(0)
	v_mfma_f32_16x16x32_bf16 v[176:179], v[188:191], v[192:195], v[176:179]
	s_waitcnt vmcnt(5)
	ds_write_b128 v75, v[196:199]
	s_waitcnt vmcnt(4)
	ds_write_b128 v75, v[204:207] offset:9216
	s_waitcnt lgkmcnt(0)
	s_barrier
	v_exp_f32_e32 v141, v9
	v_sub_f32_e32 v9, v150, v136
	ds_read2_b64 v[188:191], v8 offset1:4
	v_mul_f32_e32 v9, 0x3fb8aa3b, v9
	ds_read2_b64 v[192:195], v7 offset0:32 offset1:36
	v_exp_f32_e32 v140, v9
	v_sub_f32_e32 v9, v143, v136
	v_sub_f32_e32 v8, v146, v136
	v_mul_f32_e32 v9, 0x3fb8aa3b, v9
	v_mul_f32_e32 v8, 0x3fb8aa3b, v8
	v_exp_f32_e32 v142, v9
	v_exp_f32_e32 v143, v8
	v_cvt_pk_bf16_f32 v144, v137, v139
	v_cvt_pk_bf16_f32 v146, v135, v138
	v_cvt_pk_bf16_f32 v145, v141, v142
	v_cvt_pk_bf16_f32 v147, v140, v143
	v_lshl_add_u64 v[8:9], s[26:27], 1, v[78:79]
	v_fma_f32 v64, v64, s74, -v136
	s_waitcnt lgkmcnt(1)
	v_mfma_f32_16x16x32_bf16 v[180:183], v[188:191], v[144:147], v[180:183]
	ds_read2_b64 v[188:191], v6 offset0:64 offset1:68
	v_lshl_add_u64 v[6:7], v[8:9], 0, v[70:71]
	v_lshl_add_u64 v[8:9], v[8:9], 0, v[80:81]
	s_waitcnt lgkmcnt(1)
	v_mfma_f32_16x16x32_bf16 v[164:167], v[192:195], v[144:147], v[164:167]
	v_lshl_add_u64 v[248:249], v[6:7], 0, 0
	v_lshl_add_u64 v[238:239], v[8:9], 0, 0
	global_load_dwordx4 v[192:195], v[6:7], off
	global_load_dwordx4 v[196:199], v[8:9], off
	global_load_dword v250, v[248:249], off offset:128
	global_load_dword v251, v[238:239], off offset:128
	ds_read2_b64 v[78:81], v158 offset0:96 offset1:100
	s_waitcnt vmcnt(5)
	ds_write_b128 v75, v[184:187] offset:18432
	s_waitcnt vmcnt(4)
	ds_write_b128 v75, v[200:203] offset:27648
	s_waitcnt lgkmcnt(3)
	v_mfma_f32_16x16x32_bf16 v[172:175], v[188:191], v[144:147], v[172:175]
	s_waitcnt lgkmcnt(0)
	s_barrier
; #define LAS __attribute__((address_space(3)))
; __device__ __forceinline__ unsigned cvt_pk_bf16(float lo, float hi) { const float __attribute__((ext_vector_type(2))) v = {lo, hi}; return __builtin_bit_cast(unsigned, __builtin_convertvector(v, bf16x2_t)); }
; #define NA_STORE(sidx) do { LAS bf16* d_ = buf + ((sidx) & 1) * 9216; _Pragma("unroll") for (int q_ = 0; q_ < 2; ++q_) *(LAS v4u*)(d_ + q_ * 4608 + lrow * 72 + lseg * 8) = ld[(sidx) & 1][q_]; } while (0)
; template <bool LOCAL>
; __device__ __forceinline__ void na_unit(const bf16* P, const bf16* VT, bf16* YCAT, const LAS float* rpb_l, LAS bf16* buf, int b, int gr, int hp, int qblk, int tid) {
;     ...
;             } else {
;                 const int cc = c - NLOC;
; #pragma unroll
;                 for (int p2 = 0; p2 < 2; ++p2) {
;                     float p[8];
; #pragma unroll
;                     for (int e = 0; e < 4; ++e) { p[e] = __expf(sc[4 * (cc >= 0 ? cc : 0) + 2 * p2][e] - m); p[4 + e] = __expf(sc[4 * (cc >= 0 ? cc : 0) + 2 * p2 + 1][e] - m); }
; #pragma unroll
;                     for (int e = 0; e < 8; ++e) lsum += p[e];
;                     const bf16x8 pf = __builtin_bit_cast(bf16x8, (v4u){pg8::cvt_pk_bf16(p[0], p[1]), pg8::cvt_pk_bf16(p[2], p[3]), pg8::cvt_pk_bf16(p[4], p[5]), pg8::cvt_pk_bf16(p[6], p[7])});
; #pragma unroll
;                     for (int dt = 0; dt < 4; ++dt) { const LAS bf16* vp = cb + (16 * dt + fr) * 72 + 32 * p2 + 4 * fq;
;                         o[dt] = __builtin_amdgcn_mfma_f32_16x16x32_bf16(frag44(vp, vp + 16), pf, o[dt], 0, 0, 0); }
;                 }
;             }
;         }
;         if (sidx + 1 < 2 * NCH) NA_STORE(sidx + 1);
	v_mfma_f32_16x16x32_bf16 v[176:179], v[78:81], v[144:147], v[176:179]
	v_sub_f32_e32 v70, v149, v136
	v_sub_f32_e32 v79, v148, v136
	v_sub_f32_e32 v81, v152, v136
	v_sub_f32_e32 v145, v151, v136
	ds_read2_b64 v[148:151], v160 offset1:4
	v_mul_f32_e32 v70, 0x3fb8aa3b, v70
	v_mul_f32_e32 v79, 0x3fb8aa3b, v79
	v_mul_f32_e32 v81, 0x3fb8aa3b, v81
	v_mul_f32_e32 v145, 0x3fb8aa3b, v145
	v_exp_f32_e32 v78, v70
	v_sub_f32_e32 v70, v155, v136
	v_exp_f32_e32 v80, v79
	v_sub_f32_e32 v79, v153, v136
	v_exp_f32_e32 v144, v81
	v_sub_f32_e32 v81, v157, v136
	v_exp_f32_e32 v146, v145
	v_sub_f32_e32 v145, v154, v136
	v_mul_f32_e32 v70, 0x3fb8aa3b, v70
	v_mul_f32_e32 v79, 0x3fb8aa3b, v79
	v_mul_f32_e32 v81, 0x3fb8aa3b, v81
	v_mul_f32_e32 v145, 0x3fb8aa3b, v145
	v_exp_f32_e32 v70, v70
	v_exp_f32_e32 v79, v79
	v_exp_f32_e32 v81, v81
	v_exp_f32_e32 v145, v145
	v_cvt_pk_bf16_f32 v152, v78, v80
	v_cvt_pk_bf16_f32 v153, v144, v146
	v_cvt_pk_bf16_f32 v154, v70, v79
	v_cvt_pk_bf16_f32 v155, v81, v145
	v_fma_f32 v65, v65, s74, -v136
	v_mul_f32_e32 v62, 0x3fb8aa3b, v62
	s_waitcnt lgkmcnt(0)
	v_mfma_f32_16x16x32_bf16 v[148:151], v[148:151], v[152:155], v[180:183]
	v_mul_f32_e32 v63, 0x3fb8aa3b, v63
	v_mul_f32_e32 v64, 0x3fb8aa3b, v64
	v_mul_f32_e32 v65, 0x3fb8aa3b, v65
	ds_read2_b64 v[180:183], v159 offset0:32 offset1:36
	ds_read2_b64 v[158:161], v161 offset0:64 offset1:68
	s_waitcnt lgkmcnt(0)
	v_mfma_f32_16x16x32_bf16 v[158:161], v[158:161], v[152:155], v[172:175]
	s_nop 2
	ds_read2_b64 v[172:175], v162 offset0:96 offset1:100
	v_exp_f32_e32 v147, v62
	v_fma_f32 v62, v66, s74, -v136
	v_mfma_f32_16x16x32_bf16 v[164:167], v[180:183], v[152:155], v[164:167]
	v_lshl_add_u64 v[248:249], v[6:7], 0, 0
	v_lshl_add_u64 v[238:239], v[8:9], 0, 0
	global_load_dwordx4 v[180:183], v[6:7], off offset:128
	global_load_dwordx4 v[184:187], v[8:9], off offset:128
	global_load_dword v250, v[248:249], off offset:256
	global_load_dword v251, v[238:239], off offset:256
	s_waitcnt vmcnt(7)
	ds_write_b128 v75, v[192:195]
	s_waitcnt vmcnt(6)
	ds_write_b128 v75, v[196:199] offset:9216
	s_waitcnt lgkmcnt(0)
	v_mfma_f32_16x16x32_bf16 v[152:155], v[172:175], v[152:155], v[176:179]
	s_barrier
	ds_read2_b64 v[172:175], v156 offset1:4
	v_exp_f32_e32 v66, v63
	v_fma_f32 v63, v67, s74, -v136
	v_exp_f32_e32 v67, v64
	v_fma_f32 v64, v68, s74, -v136
	v_exp_f32_e32 v68, v65
	v_fma_f32 v65, v69, s74, -v136
	v_mul_f32_e32 v62, 0x3fb8aa3b, v62
	v_mul_f32_e32 v63, 0x3fb8aa3b, v63
	v_mul_f32_e32 v64, 0x3fb8aa3b, v64
	v_mul_f32_e32 v65, 0x3fb8aa3b, v65
	v_exp_f32_e32 v62, v62
	v_exp_f32_e32 v63, v63
	v_exp_f32_e32 v64, v64
	v_exp_f32_e32 v65, v65
	v_cvt_pk_bf16_f32 v176, v147, v66
	v_cvt_pk_bf16_f32 v177, v67, v68
	v_cvt_pk_bf16_f32 v178, v62, v63
	v_cvt_pk_bf16_f32 v179, v64, v65
	v_add_u32_e32 v157, 0x800, v156
	v_add_u32_e32 v192, 0x1000, v156
	s_waitcnt lgkmcnt(0)
	v_mfma_f32_16x16x32_bf16 v[148:151], v[172:175], v[176:179], v[148:151]
	ds_read2_b64 v[172:175], v157 offset0:32 offset1:36
	v_add_u32_e32 v193, 0x1800, v156
	v_fma_f32 v58, v58, s74, -v136
	s_waitcnt lgkmcnt(0)
	v_mfma_f32_16x16x32_bf16 v[162:165], v[172:175], v[176:179], v[164:167]
	s_nop 2
	ds_read2_b64 v[166:169], v192 offset0:64 offset1:68
	v_fma_f32 v54, v54, s74, -v136
	v_fma_f32 v59, v59, s74, -v136
	s_waitcnt lgkmcnt(0)
	v_mfma_f32_16x16x32_bf16 v[158:161], v[166:169], v[176:179], v[158:161]
	ds_read2_b64 v[166:169], v193 offset0:96 offset1:100
	v_fma_f32 v55, v55, s74, -v136
	v_fma_f32 v60, v60, s74, -v136
	s_waitcnt lgkmcnt(0)
	v_mfma_f32_16x16x32_bf16 v[152:155], v[166:169], v[176:179], v[152:155]
	ds_read2_b64 v[166:169], v156 offset0:8 offset1:12
	v_fma_f32 v56, v56, s74, -v136
	v_fma_f32 v61, v61, s74, -v136
	v_fma_f32 v57, v57, s74, -v136
	v_mul_f32_e32 v58, 0x3fb8aa3b, v58
	v_mul_f32_e32 v54, 0x3fb8aa3b, v54
	v_mul_f32_e32 v59, 0x3fb8aa3b, v59
	v_mul_f32_e32 v55, 0x3fb8aa3b, v55
	v_mul_f32_e32 v60, 0x3fb8aa3b, v60
	v_mul_f32_e32 v56, 0x3fb8aa3b, v56
	v_mul_f32_e32 v61, 0x3fb8aa3b, v61
	v_mul_f32_e32 v57, 0x3fb8aa3b, v57
	v_exp_f32_e32 v58, v58
	v_exp_f32_e32 v54, v54
	v_exp_f32_e32 v59, v59
	v_exp_f32_e32 v55, v55
	v_exp_f32_e32 v60, v60
	v_exp_f32_e32 v56, v56
	v_exp_f32_e32 v61, v61
	v_exp_f32_e32 v57, v57
	v_cvt_pk_bf16_f32 v172, v58, v59
	v_cvt_pk_bf16_f32 v174, v54, v55
	v_cvt_pk_bf16_f32 v173, v60, v61
	v_cvt_pk_bf16_f32 v175, v56, v57
	v_fma_f32 v46, v46, s74, -v136
	v_fma_f32 v47, v47, s74, -v136
	s_waitcnt lgkmcnt(0)
	v_mfma_f32_16x16x32_bf16 v[148:151], v[166:169], v[172:175], v[148:151]
	ds_read2_b64 v[166:169], v157 offset0:40 offset1:44
	v_fma_f32 v48, v48, s74, -v136
	v_mul_f32_e32 v46, 0x3fb8aa3b, v46
	s_waitcnt lgkmcnt(0)
	v_mfma_f32_16x16x32_bf16 v[162:165], v[166:169], v[172:175], v[162:165]
	ds_read2_b64 v[166:169], v192 offset0:72 offset1:76
	v_mul_f32_e32 v47, 0x3fb8aa3b, v47
	v_mul_f32_e32 v48, 0x3fb8aa3b, v48
	s_waitcnt lgkmcnt(0)
	v_mfma_f32_16x16x32_bf16 v[158:161], v[166:169], v[172:175], v[158:161]
	ds_read2_b64 v[166:169], v193 offset0:104 offset1:108
	v_exp_f32_e32 v69, v46
	v_fma_f32 v46, v50, s74, -v136
	v_exp_f32_e32 v50, v47
	v_fma_f32 v47, v51, s74, -v136
	v_exp_f32_e32 v51, v48
	v_fma_f32 v48, v52, s74, -v136
	v_add_u32_e32 v52, 0x4800, v156
	v_lshl_add_u64 v[248:249], v[6:7], 0, 0
	v_lshl_add_u64 v[238:239], v[8:9], 0, 0
	global_load_dwordx4 v[176:179], v[6:7], off offset:256
	global_load_dwordx4 v[188:191], v[8:9], off offset:256
	global_load_dword v250, v[248:249], off offset:384
	global_load_dword v251, v[238:239], off offset:384
	s_waitcnt lgkmcnt(0)
	v_mfma_f32_16x16x32_bf16 v[152:155], v[166:169], v[172:175], v[152:155]
	s_waitcnt vmcnt(7)
	ds_write_b128 v75, v[180:183] offset:18432
	s_waitcnt vmcnt(6)
	ds_write_b128 v75, v[184:187] offset:27648
	s_waitcnt lgkmcnt(0)
	s_barrier
; #define LAS __attribute__((address_space(3)))
; __device__ __forceinline__ unsigned cvt_pk_bf16(float lo, float hi) { const float __attribute__((ext_vector_type(2))) v = {lo, hi}; return __builtin_bit_cast(unsigned, __builtin_convertvector(v, bf16x2_t)); }
; #define NA_STORE(sidx) do { LAS bf16* d_ = buf + ((sidx) & 1) * 9216; _Pragma("unroll") for (int q_ = 0; q_ < 2; ++q_) *(LAS v4u*)(d_ + q_ * 4608 + lrow * 72 + lseg * 8) = ld[(sidx) & 1][q_]; } while (0)
; template <bool LOCAL>
; __device__ __forceinline__ void na_unit(const bf16* P, const bf16* VT, bf16* YCAT, const LAS float* rpb_l, LAS bf16* buf, int b, int gr, int hp, int qblk, int tid) {
;     ...
;             } else {
;                 const int cc = c - NLOC;
; #pragma unroll
;                 for (int p2 = 0; p2 < 2; ++p2) {
;                     float p[8];
; #pragma unroll
;                     for (int e = 0; e < 4; ++e) { p[e] = __expf(sc[4 * (cc >= 0 ? cc : 0) + 2 * p2][e] - m); p[4 + e] = __expf(sc[4 * (cc >= 0 ? cc : 0) + 2 * p2 + 1][e] - m); }
; #pragma unroll
;                     for (int e = 0; e < 8; ++e) lsum += p[e];
;                     const bf16x8 pf = __builtin_bit_cast(bf16x8, (v4u){pg8::cvt_pk_bf16(p[0], p[1]), pg8::cvt_pk_bf16(p[2], p[3]), pg8::cvt_pk_bf16(p[4], p[5]), pg8::cvt_pk_bf16(p[6], p[7])});
; #pragma unroll
;                     for (int dt = 0; dt < 4; ++dt) { const LAS bf16* vp = cb + (16 * dt + fr) * 72 + 32 * p2 + 4 * fq;
;                         o[dt] = __builtin_amdgcn_mfma_f32_16x16x32_bf16(frag44(vp, vp + 16), pf, o[dt], 0, 0, 0); }
;                 }
;             }
;         }
;         if (sidx + 1 < 2 * NCH) NA_STORE(sidx + 1);
;         __syncthreads();
	v_fma_f32 v49, v49, s74, -v136
	ds_read2_b64 v[166:169], v52 offset1:4
	v_mul_f32_e32 v49, 0x3fb8aa3b, v49
	v_exp_f32_e32 v180, v49
	v_fma_f32 v49, v53, s74, -v136
	v_mul_f32_e32 v46, 0x3fb8aa3b, v46
	v_mul_f32_e32 v47, 0x3fb8aa3b, v47
	v_mul_f32_e32 v48, 0x3fb8aa3b, v48
	v_mul_f32_e32 v49, 0x3fb8aa3b, v49
	v_exp_f32_e32 v46, v46
	v_exp_f32_e32 v47, v47
	v_exp_f32_e32 v48, v48
	v_exp_f32_e32 v53, v49
	v_cvt_pk_bf16_f32 v172, v69, v50
	v_cvt_pk_bf16_f32 v173, v51, v180
	v_cvt_pk_bf16_f32 v174, v46, v47
	v_cvt_pk_bf16_f32 v175, v48, v53
	v_add_u32_e32 v181, 0x5000, v156
	v_add_u32_e32 v182, 0x5800, v156
	s_waitcnt lgkmcnt(0)
	v_mfma_f32_16x16x32_bf16 v[148:151], v[166:169], v[172:175], v[148:151]
	ds_read2_b64 v[166:169], v181 offset0:32 offset1:36
	v_add_u32_e32 v49, 0x6000, v156
	v_fma_f32 v38, v38, s74, -v136
	s_waitcnt lgkmcnt(0)
	v_mfma_f32_16x16x32_bf16 v[162:165], v[166:169], v[172:175], v[162:165]
	ds_read2_b64 v[166:169], v182 offset0:64 offset1:68
	v_mul_f32_e32 v38, 0x3fb8aa3b, v38
	v_fma_f32 v42, v42, s74, -v136
	s_waitcnt lgkmcnt(0)
	v_mfma_f32_16x16x32_bf16 v[158:161], v[166:169], v[172:175], v[158:161]
	ds_read2_b64 v[166:169], v49 offset0:96 offset1:100
	v_mul_f32_e32 v42, 0x3fb8aa3b, v42
	v_fma_f32 v30, v30, s74, -v136
	s_waitcnt lgkmcnt(0)
	v_mfma_f32_16x16x32_bf16 v[152:155], v[166:169], v[172:175], v[152:155]
	v_exp_f32_e32 v173, v38
	v_fma_f32 v38, v43, s74, -v136
	v_mul_f32_e32 v38, 0x3fb8aa3b, v38
	v_exp_f32_e32 v174, v38
	v_fma_f32 v38, v39, s74, -v136
	v_mul_f32_e32 v38, 0x3fb8aa3b, v38
	v_exp_f32_e32 v175, v38
	v_fma_f32 v38, v44, s74, -v136
	v_mul_f32_e32 v38, 0x3fb8aa3b, v38
	v_exp_f32_e32 v183, v38
	v_fma_f32 v38, v40, s74, -v136
	v_mul_f32_e32 v38, 0x3fb8aa3b, v38
	v_exp_f32_e32 v172, v42
	v_exp_f32_e32 v184, v38
	v_fma_f32 v38, v45, s74, -v136
	ds_read2_b64 v[42:45], v52 offset0:8 offset1:12
	v_mul_f32_e32 v38, 0x3fb8aa3b, v38
	v_exp_f32_e32 v185, v38
	v_fma_f32 v38, v41, s74, -v136
	v_mul_f32_e32 v38, 0x3fb8aa3b, v38
	v_exp_f32_e32 v186, v38
	v_cvt_pk_bf16_f32 v38, v172, v174
	v_cvt_pk_bf16_f32 v39, v183, v185
	v_cvt_pk_bf16_f32 v40, v173, v175
	v_cvt_pk_bf16_f32 v41, v184, v186
	v_mul_f32_e32 v30, 0x3fb8aa3b, v30
	v_fma_f32 v22, v22, s74, -v136
	s_waitcnt lgkmcnt(0)
	v_mfma_f32_16x16x32_bf16 v[42:45], v[42:45], v[38:41], v[148:151]
	v_mul_f32_e32 v22, 0x3fb8aa3b, v22
	v_fma_f32 v26, v26, s74, -v136
	v_mul_f32_e32 v26, 0x3fb8aa3b, v26
	ds_read2_b64 v[148:151], v181 offset0:40 offset1:44
	s_waitcnt lgkmcnt(0)
	v_mfma_f32_16x16x32_bf16 v[148:151], v[148:151], v[38:41], v[162:165]
	s_nop 2
	ds_read2_b64 v[162:165], v182 offset0:72 offset1:76
	v_fma_f32 v2, v2, s74, -v136
	v_mul_f32_e32 v2, 0x3fb8aa3b, v2
	s_waitcnt lgkmcnt(0)
	v_mfma_f32_16x16x32_bf16 v[158:161], v[162:165], v[38:41], v[158:161]
	ds_read2_b64 v[162:165], v49 offset0:104 offset1:108
	global_load_dwordx4 v[166:169], v[6:7], off offset:384
	s_nop 0
	global_load_dwordx4 v[6:9], v[8:9], off offset:384
	s_waitcnt vmcnt(5)
	ds_write_b128 v75, v[176:179]
	s_waitcnt vmcnt(4)
	ds_write_b128 v75, v[188:191] offset:9216
	s_waitcnt lgkmcnt(2)
	v_mfma_f32_16x16x32_bf16 v[38:41], v[162:165], v[38:41], v[152:155]
	v_exp_f32_e32 v162, v30
	v_fma_f32 v30, v34, s74, -v136
	v_mul_f32_e32 v30, 0x3fb8aa3b, v30
	v_exp_f32_e32 v163, v30
	v_fma_f32 v30, v31, s74, -v136
	v_mul_f32_e32 v30, 0x3fb8aa3b, v30
	v_exp_f32_e32 v164, v30
	v_fma_f32 v30, v35, s74, -v136
	v_mul_f32_e32 v30, 0x3fb8aa3b, v30
	v_exp_f32_e32 v165, v30
	v_fma_f32 v30, v32, s74, -v136
	v_mul_f32_e32 v30, 0x3fb8aa3b, v30
	v_exp_f32_e32 v176, v30
	v_fma_f32 v30, v36, s74, -v136
	v_mul_f32_e32 v30, 0x3fb8aa3b, v30
	v_exp_f32_e32 v177, v30
	v_fma_f32 v30, v33, s74, -v136
	s_waitcnt lgkmcnt(0)
	s_barrier
	v_mul_f32_e32 v34, 0x3fb8aa3b, v30
	ds_read2_b64 v[30:33], v156 offset1:4
	v_exp_f32_e32 v178, v34
	v_fma_f32 v34, v37, s74, -v136
	v_mul_f32_e32 v34, 0x3fb8aa3b, v34
	v_exp_f32_e32 v179, v34
	v_cvt_pk_bf16_f32 v34, v162, v164
	v_cvt_pk_bf16_f32 v35, v176, v178
	v_cvt_pk_bf16_f32 v36, v163, v165
	v_cvt_pk_bf16_f32 v37, v177, v179
	ds_read2_b64 v[152:155], v193 offset0:96 offset1:100
	v_fma_f32 v10, v10, s74, -v136
	s_waitcnt lgkmcnt(1)
	v_mfma_f32_16x16x32_bf16 v[30:33], v[30:33], v[34:37], v[42:45]
	v_mul_f32_e32 v10, 0x3fb8aa3b, v10
	s_nop 1
	ds_read2_b64 v[42:45], v157 offset0:32 offset1:36
	s_waitcnt lgkmcnt(0)
	v_mfma_f32_16x16x32_bf16 v[42:45], v[42:45], v[34:37], v[148:151]
	s_nop 2
	ds_read2_b64 v[148:151], v192 offset0:64 offset1:68
	s_waitcnt lgkmcnt(0)
	v_mfma_f32_16x16x32_bf16 v[148:151], v[148:151], v[34:37], v[158:161]
	v_mfma_f32_16x16x32_bf16 v[34:37], v[152:155], v[34:37], v[38:41]
	v_exp_f32_e32 v153, v22
	v_fma_f32 v22, v27, s74, -v136
	v_mul_f32_e32 v22, 0x3fb8aa3b, v22
	v_exp_f32_e32 v154, v22
	v_fma_f32 v22, v23, s74, -v136
	v_mul_f32_e32 v22, 0x3fb8aa3b, v22
	v_exp_f32_e32 v155, v22
	v_fma_f32 v22, v28, s74, -v136
	v_mul_f32_e32 v22, 0x3fb8aa3b, v22
	v_exp_f32_e32 v158, v22
	v_fma_f32 v22, v24, s74, -v136
	v_mul_f32_e32 v22, 0x3fb8aa3b, v22
	v_exp_f32_e32 v152, v26
	v_exp_f32_e32 v159, v22
	v_fma_f32 v22, v29, s74, -v136
	ds_read2_b64 v[26:29], v156 offset0:8 offset1:12
	v_mul_f32_e32 v22, 0x3fb8aa3b, v22
	v_exp_f32_e32 v156, v22
	v_fma_f32 v22, v25, s74, -v136
	v_mul_f32_e32 v22, 0x3fb8aa3b, v22
	v_exp_f32_e32 v160, v22
	v_cvt_pk_bf16_f32 v22, v152, v154
	v_cvt_pk_bf16_f32 v23, v158, v156
	v_cvt_pk_bf16_f32 v24, v153, v155
	v_cvt_pk_bf16_f32 v25, v159, v160
	ds_read2_b64 v[38:41], v192 offset0:72 offset1:76
	s_waitcnt lgkmcnt(1)
	v_mfma_f32_16x16x32_bf16 v[26:29], v[26:29], v[22:25], v[30:33]
	s_nop 2
	ds_read2_b64 v[30:33], v157 offset0:40 offset1:44
	s_waitcnt lgkmcnt(0)
	v_mfma_f32_16x16x32_bf16 v[30:33], v[30:33], v[22:25], v[42:45]
	s_nop 2
	ds_read2_b64 v[42:45], v193 offset0:104 offset1:108
	s_waitcnt vmcnt(1)
	ds_write_b128 v75, v[166:169] offset:18432
	s_waitcnt vmcnt(0)
	ds_write_b128 v75, v[6:9] offset:27648
	v_fma_f32 v6, v14, s74, -v136
	v_mul_f32_e32 v6, 0x3fb8aa3b, v6
	v_mfma_f32_16x16x32_bf16 v[38:41], v[38:41], v[22:25], v[148:151]
	s_waitcnt lgkmcnt(0)
	s_barrier
; #define LAS __attribute__((address_space(3)))
; __device__ __forceinline__ unsigned cvt_pk_bf16(float lo, float hi) { const float __attribute__((ext_vector_type(2))) v = {lo, hi}; return __builtin_bit_cast(unsigned, __builtin_convertvector(v, bf16x2_t)); }
; #define NA_STORE(sidx) do { LAS bf16* d_ = buf + ((sidx) & 1) * 9216; _Pragma("unroll") for (int q_ = 0; q_ < 2; ++q_) *(LAS v4u*)(d_ + q_ * 4608 + lrow * 72 + lseg * 8) = ld[(sidx) & 1][q_]; } while (0)
; template <bool LOCAL>
; __device__ __forceinline__ void na_unit(const bf16* P, const bf16* VT, bf16* YCAT, const LAS float* rpb_l, LAS bf16* buf, int b, int gr, int hp, int qblk, int tid) {
;     ...
;                 const int cc = c - NLOC;
; #pragma unroll
;                 for (int p2 = 0; p2 < 2; ++p2) {
;                     float p[8];
; #pragma unroll
;                     for (int e = 0; e < 4; ++e) { p[e] = __expf(sc[4 * (cc >= 0 ? cc : 0) + 2 * p2][e] - m); p[4 + e] = __expf(sc[4 * (cc >= 0 ? cc : 0) + 2 * p2 + 1][e] - m); }
; #pragma unroll
;                     for (int e = 0; e < 8; ++e) lsum += p[e];
;                     const bf16x8 pf = __builtin_bit_cast(bf16x8, (v4u){pg8::cvt_pk_bf16(p[0], p[1]), pg8::cvt_pk_bf16(p[2], p[3]), pg8::cvt_pk_bf16(p[4], p[5]), pg8::cvt_pk_bf16(p[6], p[7])});
; #pragma unroll
;                     for (int dt = 0; dt < 4; ++dt) { const LAS bf16* vp = cb + (16 * dt + fr) * 72 + 32 * p2 + 4 * fq;
;                         o[dt] = __builtin_amdgcn_mfma_f32_16x16x32_bf16(frag44(vp, vp + 16), pf, o[dt], 0, 0, 0); }
;                 }
;             }
;         }
;         if (sidx + 1 < 2 * NCH) NA_STORE(sidx + 1);
;         __syncthreads();
;     }
;     ...
;     lsum += __shfl_xor(lsum, 16); lsum += __shfl_xor(lsum, 32);
	v_mfma_f32_16x16x32_bf16 v[22:25], v[42:45], v[22:25], v[34:37]
	v_ashrrev_i32_e32 v75, 31, v74
	s_nop 1
	v_exp_f32_e32 v34, v6
	v_fma_f32 v6, v18, s74, -v136
	v_mul_f32_e32 v6, 0x3fb8aa3b, v6
	v_exp_f32_e32 v35, v6
	v_fma_f32 v6, v15, s74, -v136
	v_mul_f32_e32 v6, 0x3fb8aa3b, v6
	v_exp_f32_e32 v36, v6
	v_fma_f32 v6, v19, s74, -v136
	v_mul_f32_e32 v6, 0x3fb8aa3b, v6
	v_exp_f32_e32 v37, v6
	v_fma_f32 v6, v16, s74, -v136
	v_mul_f32_e32 v6, 0x3fb8aa3b, v6
	v_exp_f32_e32 v42, v6
	v_fma_f32 v6, v20, s74, -v136
	v_mul_f32_e32 v6, 0x3fb8aa3b, v6
	v_exp_f32_e32 v43, v6
	v_fma_f32 v6, v17, s74, -v136
	v_mul_f32_e32 v14, 0x3fb8aa3b, v6
	ds_read2_b64 v[6:9], v52 offset1:4
	v_exp_f32_e32 v44, v14
	v_fma_f32 v14, v21, s74, -v136
	v_mul_f32_e32 v14, 0x3fb8aa3b, v14
	v_exp_f32_e32 v45, v14
	v_cvt_pk_bf16_f32 v14, v34, v36
	v_cvt_pk_bf16_f32 v15, v42, v44
	v_cvt_pk_bf16_f32 v16, v35, v37
	v_cvt_pk_bf16_f32 v17, v43, v45
	ds_read2_b64 v[18:21], v181 offset0:32 offset1:36
	s_waitcnt lgkmcnt(1)
	v_mfma_f32_16x16x32_bf16 v[6:9], v[6:9], v[14:17], v[26:29]
	s_nop 2
	ds_read2_b64 v[26:29], v182 offset0:64 offset1:68
	s_waitcnt lgkmcnt(0)
	v_mfma_f32_16x16x32_bf16 v[26:29], v[26:29], v[14:17], v[38:41]
	s_nop 2
	v_add_f32_e32 v38, 0, v132
	v_add_f32_e32 v38, v96, v38
	v_add_f32_e32 v38, v95, v38
	v_add_f32_e32 v38, v99, v38
	v_add_f32_e32 v38, v92, v38
	v_add_f32_e32 v38, v91, v38
	v_add_f32_e32 v38, v94, v38
	v_add_f32_e32 v38, v93, v38
	v_add_f32_e32 v38, v86, v38
	v_add_f32_e32 v38, v90, v38
	v_add_f32_e32 v38, v98, v38
	v_add_f32_e32 v38, v100, v38
	v_add_f32_e32 v38, v76, v38
	v_add_f32_e32 v38, v87, v38
	v_add_f32_e32 v38, v97, v38
	v_add_f32_e32 v38, v101, v38
	v_add_f32_e32 v38, v103, v38
	v_add_f32_e32 v38, v105, v38
	v_add_f32_e32 v38, v107, v38
	v_add_f32_e32 v38, v108, v38
	v_add_f32_e32 v38, v102, v38
	v_add_f32_e32 v38, v104, v38
	v_add_f32_e32 v38, v106, v38
	v_add_f32_e32 v38, v109, v38
	v_add_f32_e32 v38, v111, v38
	v_add_f32_e32 v38, v113, v38
	v_add_f32_e32 v38, v115, v38
	v_add_f32_e32 v38, v116, v38
	v_add_f32_e32 v38, v110, v38
	v_add_f32_e32 v38, v112, v38
	v_add_f32_e32 v38, v114, v38
	v_add_f32_e32 v38, v117, v38
	v_add_f32_e32 v38, v119, v38
	v_add_f32_e32 v38, v121, v38
	v_add_f32_e32 v38, v123, v38
	v_add_f32_e32 v38, v124, v38
	v_add_f32_e32 v38, v118, v38
	v_add_f32_e32 v38, v120, v38
	v_add_f32_e32 v38, v122, v38
	v_add_f32_e32 v38, v125, v38
	v_add_f32_e32 v38, v127, v38
	v_add_f32_e32 v38, v129, v38
	v_add_f32_e32 v38, v131, v38
	v_add_f32_e32 v38, v133, v38
	v_add_f32_e32 v38, v126, v38
	v_add_f32_e32 v38, v128, v38
	v_add_f32_e32 v38, v130, v38
	v_add_f32_e32 v38, v134, v38
	v_add_f32_e32 v38, v137, v38
	v_add_f32_e32 v38, v139, v38
	v_add_f32_e32 v38, v141, v38
	v_add_f32_e32 v38, v142, v38
	v_add_f32_e32 v38, v135, v38
	v_add_f32_e32 v38, v138, v38
	v_add_f32_e32 v38, v140, v38
	v_add_f32_e32 v38, v143, v38
	v_add_f32_e32 v38, v78, v38
	v_add_f32_e32 v38, v80, v38
	v_add_f32_e32 v38, v144, v38
	v_add_f32_e32 v38, v146, v38
	v_add_f32_e32 v38, v70, v38
	v_add_f32_e32 v38, v79, v38
	v_add_f32_e32 v38, v81, v38
	v_add_f32_e32 v38, v145, v38
	v_add_f32_e32 v38, v147, v38
	v_add_f32_e32 v38, v66, v38
	v_add_f32_e32 v38, v67, v38
	v_add_f32_e32 v38, v68, v38
	v_add_f32_e32 v38, v62, v38
	v_add_f32_e32 v38, v63, v38
	v_add_f32_e32 v38, v64, v38
	v_add_f32_e32 v38, v65, v38
	v_add_f32_e32 v38, v58, v38
	v_add_f32_e32 v38, v59, v38
	v_add_f32_e32 v38, v60, v38
	v_add_f32_e32 v38, v61, v38
	v_add_f32_e32 v38, v54, v38
	v_add_f32_e32 v38, v55, v38
	v_add_f32_e32 v38, v56, v38
	v_add_f32_e32 v38, v57, v38
	v_add_f32_e32 v38, v69, v38
	v_add_f32_e32 v38, v50, v38
	v_add_f32_e32 v38, v51, v38
	v_add_f32_e32 v38, v180, v38
	v_add_f32_e32 v38, v46, v38
	v_add_f32_e32 v38, v47, v38
	v_add_f32_e32 v38, v48, v38
	v_add_f32_e32 v38, v53, v38
	v_add_f32_e32 v38, v172, v38
	v_mfma_f32_16x16x32_bf16 v[18:21], v[18:21], v[14:17], v[30:33]
	v_add_f32_e32 v38, v174, v38
	v_add_f32_e32 v38, v183, v38
	v_add_f32_e32 v38, v185, v38
	ds_read2_b64 v[30:33], v49 offset0:96 offset1:100
	v_add_f32_e32 v38, v173, v38
	v_add_f32_e32 v38, v175, v38
	v_add_f32_e32 v38, v184, v38
	v_add_f32_e32 v38, v186, v38
	v_add_f32_e32 v38, v162, v38
	v_add_f32_e32 v38, v164, v38
	s_waitcnt lgkmcnt(0)
	v_mfma_f32_16x16x32_bf16 v[14:17], v[30:33], v[14:17], v[22:25]
	v_add_f32_e32 v38, v176, v38
	s_nop 1
	v_exp_f32_e32 v23, v2
	v_fma_f32 v2, v11, s74, -v136
	v_mul_f32_e32 v2, 0x3fb8aa3b, v2
	v_add_f32_e32 v38, v178, v38
	v_exp_f32_e32 v24, v2
	v_fma_f32 v2, v3, s74, -v136
	v_add_f32_e32 v38, v163, v38
	v_mul_f32_e32 v2, 0x3fb8aa3b, v2
	v_add_f32_e32 v38, v165, v38
	v_exp_f32_e32 v25, v2
	v_fma_f32 v2, v12, s74, -v136
	v_add_f32_e32 v38, v177, v38
	v_mul_f32_e32 v2, 0x3fb8aa3b, v2
	v_add_f32_e32 v38, v179, v38
	v_exp_f32_e32 v30, v2
	v_fma_f32 v2, v4, s74, -v136
	v_add_f32_e32 v38, v152, v38
	v_mul_f32_e32 v2, 0x3fb8aa3b, v2
	v_add_f32_e32 v38, v154, v38
	v_exp_f32_e32 v22, v10
	v_exp_f32_e32 v31, v2
	v_fma_f32 v2, v13, s74, -v136
	ds_read2_b64 v[10:13], v52 offset0:8 offset1:12
	v_add_f32_e32 v38, v158, v38
	v_mul_f32_e32 v2, 0x3fb8aa3b, v2
	v_add_f32_e32 v38, v156, v38
	v_exp_f32_e32 v32, v2
	v_fma_f32 v2, v5, s74, -v136
	v_add_f32_e32 v38, v153, v38
	v_mul_f32_e32 v2, 0x3fb8aa3b, v2
	v_add_f32_e32 v38, v155, v38
	v_exp_f32_e32 v33, v2
	v_add_f32_e32 v38, v159, v38
	v_add_f32_e32 v38, v160, v38
	v_add_f32_e32 v34, v34, v38
	v_add_f32_e32 v34, v36, v34
	v_cvt_pk_bf16_f32 v2, v22, v24
	v_cvt_pk_bf16_f32 v3, v30, v32
	v_cvt_pk_bf16_f32 v4, v23, v25
	v_cvt_pk_bf16_f32 v5, v31, v33
	v_add_f32_e32 v34, v42, v34
	v_add_f32_e32 v34, v44, v34
	s_waitcnt lgkmcnt(0)
	v_mfma_f32_16x16x32_bf16 v[6:9], v[10:13], v[2:5], v[6:9]
	ds_read2_b64 v[10:13], v181 offset0:40 offset1:44
	v_add_f32_e32 v34, v35, v34
	v_add_f32_e32 v34, v37, v34
	v_add_f32_e32 v34, v43, v34
	v_add_f32_e32 v34, v45, v34
	v_add_f32_e32 v22, v22, v34
	v_add_f32_e32 v22, v24, v22
	v_add_f32_e32 v22, v30, v22
	v_add_f32_e32 v22, v32, v22
	s_waitcnt lgkmcnt(0)
	v_mfma_f32_16x16x32_bf16 v[10:13], v[10:13], v[2:5], v[18:21]
	v_add_f32_e32 v22, v23, v22
	v_add_f32_e32 v22, v25, v22
	v_add_f32_e32 v22, v31, v22
	ds_read2_b64 v[18:21], v182 offset0:72 offset1:76
	v_add_f32_e32 v30, v33, v22
	ds_bpermute_b32 v31, v88, v30
	ds_read2_b64 v[22:25], v49 offset0:104 offset1:108
	s_waitcnt lgkmcnt(2)
	v_mfma_f32_16x16x32_bf16 v[18:21], v[18:21], v[2:5], v[26:29]
	s_waitcnt lgkmcnt(1)
	s_nop 1
	v_add_f32_e32 v26, v30, v31
	ds_bpermute_b32 v27, v89, v26
	v_lshlrev_b32_e32 v70, 1, v77
	s_waitcnt lgkmcnt(1)
	v_mfma_f32_16x16x32_bf16 v[14:17], v[22:25], v[2:5], v[14:17]
	s_waitcnt lgkmcnt(0)
	s_barrier
; __device__ __forceinline__ unsigned cvt_pk_bf16(float lo, float hi) { const float __attribute__((ext_vector_type(2))) v = {lo, hi}; return __builtin_bit_cast(unsigned, __builtin_convertvector(v, bf16x2_t)); }
; template <bool LOCAL>
; __device__ __forceinline__ void na_unit(const bf16* P, const bf16* VT, bf16* YCAT, const LAS float* rpb_l, LAS bf16* buf, int b, int gr, int hp, int qblk, int tid) {
;     ...
;     lsum += __shfl_xor(lsum, 16); lsum += __shfl_xor(lsum, 32);
;     const float inv = 1.f / lsum;
;     bf16* op = YCAT + (size_t)(qrow0 + fr) * D + 512 + h * 64 + 4 * fq;
; #pragma unroll
;     for (int dt = 0; dt < 4; ++dt) { v2u w; w.x = pg8::cvt_pk_bf16(o[dt][0] * inv, o[dt][1] * inv); w.y = pg8::cvt_pk_bf16(o[dt][2] * inv, o[dt][3] * inv); *(v2u*)(op + dt * 16) = w; }
	v_add_f32_e32 v2, v26, v27
	v_div_scale_f32 v3, s[0:1], v2, v2, 1.0
	v_rcp_f32_e32 v4, v3
	s_nop 0
	v_fma_f32 v5, -v3, v4, 1.0
	v_fmac_f32_e32 v4, v5, v4
	v_div_scale_f32 v5, vcc, 1.0, v2, 1.0
	v_mul_f32_e32 v22, v5, v4
	v_fma_f32 v23, -v3, v22, v5
	v_fmac_f32_e32 v22, v23, v4
	v_fma_f32 v3, -v3, v22, v5
	v_div_fmas_f32 v3, v3, v4, v22
	v_div_fixup_f32 v22, v3, v2, 1.0
	v_lshlrev_b64 v[2:3], 11, v[74:75]
	v_lshl_add_u64 v[2:3], s[10:11], 0, v[2:3]
	v_lshl_add_u64 v[2:3], v[72:73], 1, v[2:3]
	v_pk_mul_f32 v[6:7], v[6:7], v[22:23] op_sel_hi:[1,0]
	v_pk_mul_f32 v[8:9], v[8:9], v[22:23] op_sel_hi:[1,0]
	v_lshl_add_u64 v[4:5], v[2:3], 0, v[70:71]
	v_cvt_pk_bf16_f32 v6, v6, v7
	v_cvt_pk_bf16_f32 v7, v8, v9
	global_store_dwordx2 v[4:5], v[6:7], off offset:1024
	v_pk_mul_f32 v[6:7], v[10:11], v[22:23] op_sel_hi:[1,0]
	v_pk_mul_f32 v[8:9], v[12:13], v[22:23] op_sel_hi:[1,0]
	v_cvt_pk_bf16_f32 v6, v6, v7
	v_cvt_pk_bf16_f32 v7, v8, v9
	global_store_dwordx2 v[4:5], v[6:7], off offset:1056
	v_pk_mul_f32 v[6:7], v[18:19], v[22:23] op_sel_hi:[1,0]
	v_pk_mul_f32 v[8:9], v[20:21], v[22:23] op_sel_hi:[1,0]
	v_cvt_pk_bf16_f32 v6, v6, v7
	v_cvt_pk_bf16_f32 v7, v8, v9
	v_lshl_add_u64 v[2:3], v[4:5], 0, s[12:13]
	global_store_dwordx2 v[4:5], v[6:7], off offset:1088
	v_pk_mul_f32 v[4:5], v[14:15], v[22:23] op_sel_hi:[1,0]
	v_pk_mul_f32 v[6:7], v[16:17], v[22:23] op_sel_hi:[1,0]
	v_cvt_pk_bf16_f32 v4, v4, v5

; #define LAS __attribute__((address_space(3)))
; #define NA_STORE(sidx) do { LAS bf16* d_ = buf + ((sidx) & 1) * 9216; _Pragma("unroll") for (int q_ = 0; q_ < 2; ++q_) *(LAS v4u*)(d_ + q_ * 4608 + lrow * 72 + lseg * 8) = ld[(sidx) & 1][q_]; } while (0)
; template <bool LOCAL>
; __device__ __forceinline__ void na_unit(const bf16* P, const bf16* VT, bf16* YCAT, const LAS float* rpb_l, LAS bf16* buf, int b, int gr, int hp, int qblk, int tid) {
;     ...
;     const int lane = tid & 63, wv = tid >> 6, fr = lane & 15, fq = lane >> 4, hh = wv >> 2, qb = wv & 3, h = 2 * hp + hh;
;     const int qrow0 = LOCAL ? NCTX + b * SEQ + gr * 64 + 16 * qb : b * CTXL + qblk * 64 + 16 * qb;
;     const int r0 = min(max(gr - 4, 0), 24);
;     const int kc0 = qb == 0 ? 0 : qb == 1 ? 8 : qb == 2 ? 24 : 32;
;     const int qcol = 16 * qb + fr, cs = min(max(qcol - 8, 0), 48);
;     const LAS float* rpb = rpb_l + h * 15 * 31;
;     v4u ld[2][2];
;     const int lrow = (tid >> 3) & 63, lseg = tid & 7;
;     ...
;     bf16x8 qf[2];
; #pragma unroll
;     for (int ks = 0; ks < 2; ++ks) qf[ks] = *(const bf16x8*)(P + (size_t)(qrow0 + fr) * DINP + h * 64 + 32 * ks + 8 * fq);
;     f32x4 sl[16], sc[16];
;     float m = -1.0e30f, lsum = 0.f;
;     f32x4 o[4];
; #pragma unroll
;     for (int dt = 0; dt < 4; ++dt) o[dt] = (f32x4){0.f, 0.f, 0.f, 0.f};
;     NA_ISSUE(0); NA_ISSUE(1); NA_STORE(0);
;     __syncthreads();
; #pragma unroll
;     for (int sidx = 0; sidx < 2 * NCH; ++sidx) {
;         if (sidx + 2 < 2 * NCH) NA_ISSUE(sidx + 2);
;     ...
;                 for (int t4 = 0; t4 < 4; ++t4) {
;                     const LAS bf16* kp = cb + (16 * t4 + fr) * 72 + 8 * fq;
;                     f32x4 acc = {0.f, 0.f, 0.f, 0.f};
;                     acc = __builtin_amdgcn_mfma_f32_16x16x32_bf16(*(const LAS bf16x8*)(kp), qf[0], acc, 0, 0, 0);
;                     acc = __builtin_amdgcn_mfma_f32_16x16x32_bf16(*(const LAS bf16x8*)(kp + 32), qf[1], acc, 0, 0, 0);
; #pragma unroll
;                     for (int e = 0; e < 4; ++e) { acc[e] *= 0.125f; m = fmaxf(m, acc[e]); }
;                     sc[4 * (cc >= 0 ? cc : 0) + t4] = acc; }
;             }
.LBB0_3753:
	v_mov_b32_e32 v93, v0
	s_mov_b64 s[0:1], -1
	v_and_b32_e32 v89, 15, v93
	v_bfe_u32 v91, v93, 4, 2
	v_ashrrev_i32_e32 v92, 8, v93
	s_cmpk_gt_i32 s72, 0x7ff
	v_bfe_u32 v88, v93, 3, 6
	v_lshlrev_b32_e32 v76, 3, v91
	v_lshlrev_b32_e32 v70, 4, v91
	v_mad_i32_i24 v86, v92, s65, 0
	v_mul_u32_u24_e32 v87, 0x90, v89
	s_waitcnt lgkmcnt(0)
	s_barrier
	s_cbranch_scc0 .LBB0_3755
	s_lshl_b32 s0, s72, 4
	s_and_b32 s0, s0, 0xffffff00
	s_addk_i32 s0, 0x8000
	v_mov_b64_e32 v[78:79], s[8:9]
	s_lshl_b32 s1, s72, 5
	v_or_b32_e32 v77, s0, v88
	v_lshlrev_b32_e32 v4, 4, v93
	s_and_b32 s16, s1, 0x180
	v_mad_u64_u32 v[2:3], s[14:15], v77, s57, v[78:79]
	v_and_b32_e32 v80, 0x70, v4
	v_mov_b32_e32 v81, v71
	v_lshl_add_u64 v[2:3], v[2:3], 0, v[80:81]
	s_lshl_b32 s2, s16, 1
	v_lshl_add_u64 v[2:3], v[2:3], 0, s[2:3]
	global_load_dwordx4 v[6:9], v[2:3], off offset:1024
	global_load_dwordx4 v[10:13], v[2:3], off offset:1152
	s_lshl_b32 s1, s72, 6
	s_and_b32 s1, s1, 0xc0
	v_lshrrev_b32_e32 v2, 2, v93
	v_and_or_b32 v2, v2, 48, s1
	v_lshl_add_u32 v4, v92, 6, s16
	v_or3_b32 v72, v2, v89, s0
	v_ashrrev_i32_e32 v5, 31, v4
	v_mad_u64_u32 v[2:3], s[14:15], v72, s57, v[78:79]
	v_lshlrev_b64 v[74:75], 1, v[4:5]
	v_lshl_add_u64 v[2:3], v[2:3], 0, v[74:75]
	v_or_b32_e32 v14, 64, v77
	v_lshl_add_u64 v[22:23], v[2:3], 0, v[70:71]
	v_mad_u64_u32 v[14:15], s[14:15], v14, s57, v[78:79]
	global_load_dwordx4 v[2:5], v[22:23], off
	v_lshl_add_u64 v[14:15], v[14:15], 0, v[80:81]
	v_lshl_add_u64 v[18:19], v[14:15], 0, s[2:3]
	s_mov_b32 s100, 0x60000
	s_mov_b32 s101, 0
	v_lshl_add_u64 v[248:249], v[18:19], 0, s[100:101]
	global_load_dwordx4 v[14:17], v[18:19], off offset:1024
	s_nop 0
	global_load_dwordx4 v[18:21], v[18:19], off offset:1152
	global_load_dword v250, v[248:249], off offset:1024
	global_load_dword v251, v[248:249], off offset:1152
	s_nop 0
	global_load_dwordx4 v[50:53], v[22:23], off offset:64
	v_mul_u32_u24_e32 v22, 0x90, v88
	v_add3_u32 v73, 0, v22, v80
	v_or_b32_e32 v22, 0x80, v77
	v_add3_u32 v90, v86, v70, v87
	s_mov_b32 s1, s3
	v_cmp_lt_i32_e32 vcc, v83, v84
	s_waitcnt vmcnt(7)
	ds_write_b128 v73, v[6:9]
	s_waitcnt vmcnt(6)
	ds_write_b128 v73, v[10:13] offset:9216
	v_mad_u64_u32 v[10:11], s[14:15], v22, s57, v[78:79]
	v_lshl_add_u64 v[10:11], v[10:11], 0, v[80:81]
	v_lshl_add_u64 v[26:27], v[10:11], 0, s[2:3]
	s_waitcnt lgkmcnt(0)
	s_barrier
	ds_read_b128 v[6:9], v90
	ds_read_b128 v[10:13], v90 offset:2304
	v_lshl_add_u64 v[248:249], v[26:27], 0, s[100:101]
	global_load_dwordx4 v[22:25], v[26:27], off offset:1024
	global_load_dwordx4 v[30:33], v[26:27], off offset:1152
	global_load_dword v250, v[248:249], off offset:1024
	global_load_dword v251, v[248:249], off offset:1152
	ds_read_b128 v[26:29], v90 offset:64
	ds_read_b128 v[34:37], v90 offset:4608
	ds_read_b128 v[38:41], v90 offset:2368
	ds_read_b128 v[42:45], v90 offset:4672
	ds_read_b128 v[46:49], v90 offset:6912
	s_waitcnt vmcnt(9) lgkmcnt(6)
	v_mfma_f32_16x16x32_bf16 v[6:9], v[6:9], v[2:5], 0
	ds_read_b128 v[54:57], v90 offset:6976
	s_waitcnt vmcnt(8)
	ds_write_b128 v73, v[14:17] offset:18432
	s_waitcnt vmcnt(7)
	ds_write_b128 v73, v[18:21] offset:27648
	s_waitcnt lgkmcnt(0)
	v_mfma_f32_16x16x32_bf16 v[10:13], v[10:13], v[2:5], 0
	s_barrier
	v_mfma_f32_16x16x32_bf16 v[14:17], v[34:37], v[2:5], 0
	v_mfma_f32_16x16x32_bf16 v[18:21], v[46:49], v[2:5], 0
	ds_read_b128 v[34:37], v90 offset:18432
	ds_read_b128 v[46:49], v90 offset:18496
	ds_read_b128 v[58:61], v90 offset:20736
	ds_read_b128 v[94:97], v90 offset:20800
	s_waitcnt vmcnt(4)
	v_mfma_f32_16x16x32_bf16 v[62:65], v[26:29], v[50:53], v[6:9]
	s_nop 2
	v_or_b32_e32 v6, s16, v88
	s_waitcnt lgkmcnt(1)
	v_mfma_f32_16x16x32_bf16 v[98:101], v[58:61], v[2:5], 0
	ds_read_b128 v[58:61], v90 offset:23040
	ds_read_b128 v[102:105], v90 offset:23104
	v_mul_u32_u24_e32 v8, 0x9000, v6
	v_mov_b32_e32 v7, v71
	v_mfma_f32_16x16x32_bf16 v[66:69], v[38:41], v[50:53], v[10:13]
	v_mov_b32_e32 v9, v71
	s_nop 1
	v_lshl_add_u64 v[10:11], s[4:5], 0, v[80:81]
	v_or_b32_e32 v12, 64, v6
	v_or_b32_e32 v13, 0xc0, v77
	v_lshl_add_u64 v[10:11], s[0:1], 1, v[10:11]
	v_lshlrev_b32_e32 v6, 1, v8
	v_mul_u32_u24_e32 v8, 0x9000, v12
	v_mad_u64_u32 v[12:13], s[0:1], v13, s57, v[78:79]
	v_lshl_add_u64 v[78:79], v[10:11], 0, v[6:7]
	v_lshlrev_b32_e32 v8, 1, v8
	v_lshl_add_u64 v[6:7], v[12:13], 0, v[80:81]
	v_lshl_add_u64 v[80:81], v[10:11], 0, v[8:9]
	v_lshl_add_u64 v[10:11], v[6:7], 0, s[2:3]
	s_waitcnt lgkmcnt(1)
	v_mfma_f32_16x16x32_bf16 v[106:109], v[58:61], v[2:5], 0
	ds_read_b128 v[58:61], v90 offset:25344
	ds_read_b128 v[110:113], v90 offset:25408
	global_load_dwordx4 v[6:9], v[10:11], off offset:1024
	s_nop 0
	global_load_dwordx4 v[10:13], v[10:11], off offset:1152
	v_mul_f32_e32 v38, 0x3e000000, v68
	s_waitcnt lgkmcnt(1)
	v_mfma_f32_16x16x32_bf16 v[114:117], v[58:61], v[2:5], 0
	v_mul_f32_e32 v39, 0x3e000000, v69
	s_waitcnt vmcnt(5)
	ds_write_b128 v73, v[22:25]
	s_waitcnt vmcnt(4)
	ds_write_b128 v73, v[30:33] offset:9216
	v_mfma_f32_16x16x32_bf16 v[58:61], v[42:45], v[50:53], v[14:17]
	s_waitcnt lgkmcnt(0)
	s_barrier
; #define LAS __attribute__((address_space(3)))
; template <bool LOCAL>
; __device__ __forceinline__ void na_unit(const bf16* P, const bf16* VT, bf16* YCAT, const LAS float* rpb_l, LAS bf16* buf, int b, int gr, int hp, int qblk, int tid) {
;     ...
;                 for (int t4 = 0; t4 < 4; ++t4) {
;                     const LAS bf16* kp = cb + (16 * t4 + fr) * 72 + 8 * fq;
;                     f32x4 acc = {0.f, 0.f, 0.f, 0.f};
;                     acc = __builtin_amdgcn_mfma_f32_16x16x32_bf16(*(const LAS bf16x8*)(kp), qf[0], acc, 0, 0, 0);
;                     acc = __builtin_amdgcn_mfma_f32_16x16x32_bf16(*(const LAS bf16x8*)(kp + 32), qf[1], acc, 0, 0, 0);
; #pragma unroll
;                     for (int e = 0; e < 4; ++e) { acc[e] *= 0.125f; m = fmaxf(m, acc[e]); }
;                     sc[4 * (cc >= 0 ? cc : 0) + t4] = acc; }
;             }
;             if (sidx == NCH - 1) { m = fmaxf(m, __shfl_xor(m, 16)); m = fmaxf(m, __shfl_xor(m, 32)); }
	s_nop 0
	v_mul_f32_e32 v14, 0x3e000000, v62
	v_mul_f32_e32 v15, 0x3e000000, v63
	v_mfma_f32_16x16x32_bf16 v[54:57], v[54:57], v[50:53], v[18:21]
	s_nop 1
	v_mul_f32_e32 v40, 0x3e000000, v58
	v_mul_f32_e32 v41, 0x3e000000, v59
	v_mul_f32_e32 v77, 0x3e000000, v60
	v_mfma_f32_16x16x32_bf16 v[42:45], v[94:97], v[50:53], v[98:101]
	v_mul_f32_e32 v18, 0x3e000000, v64
	v_mul_f32_e32 v19, 0x3e000000, v65
	v_mul_f32_e32 v20, 0x3e000000, v66
	v_max3_f32 v99, v14, s67, v15
	v_mul_f32_e32 v21, 0x3e000000, v67
	v_max3_f32 v18, v99, v18, v19
	v_mfma_f32_16x16x32_bf16 v[34:37], v[34:37], v[2:5], 0
	v_max3_f32 v18, v18, v20, v21
	ds_read_b128 v[14:17], v90
	v_max3_f32 v22, v18, v38, v39
	ds_read_b128 v[18:21], v90 offset:2304
	v_mul_f32_e32 v94, 0x3e000000, v61
	v_max3_f32 v22, v22, v40, v41
	v_mul_f32_e32 v95, 0x3e000000, v54
	v_mul_f32_e32 v96, 0x3e000000, v55
	v_max3_f32 v38, v22, v77, v94
	v_mfma_f32_16x16x32_bf16 v[46:49], v[46:49], v[50:53], v[34:37]
	v_mul_f32_e32 v97, 0x3e000000, v56
	v_mul_f32_e32 v98, 0x3e000000, v57
	v_max3_f32 v38, v38, v95, v96
	ds_read_b128 v[22:25], v90 offset:64
	ds_read_b128 v[30:33], v90 offset:4608
	v_max3_f32 v38, v38, v97, v98
	ds_read_b128 v[94:97], v90 offset:2368
	v_mfma_f32_16x16x32_bf16 v[34:37], v[102:105], v[50:53], v[106:109]
	v_mul_f32_e32 v100, 0x3e000000, v46
	v_mul_f32_e32 v101, 0x3e000000, v47
	v_mul_f32_e32 v102, 0x3e000000, v48
	v_mul_f32_e32 v103, 0x3e000000, v49
	v_max3_f32 v38, v38, v100, v101
	v_mul_f32_e32 v106, 0x3e000000, v42
	v_mul_f32_e32 v107, 0x3e000000, v43
	s_waitcnt lgkmcnt(4)
	v_mfma_f32_16x16x32_bf16 v[14:17], v[14:17], v[2:5], 0
	v_max3_f32 v38, v38, v102, v103
	v_mul_f32_e32 v108, 0x3e000000, v44
	v_mul_f32_e32 v109, 0x3e000000, v45
	s_waitcnt lgkmcnt(3)
	v_mfma_f32_16x16x32_bf16 v[18:21], v[18:21], v[2:5], 0
	ds_read_b128 v[98:101], v90 offset:4672
	s_waitcnt lgkmcnt(2)
	v_mfma_f32_16x16x32_bf16 v[102:105], v[30:33], v[2:5], 0
	v_max3_f32 v30, v38, v106, v107
	v_max3_f32 v30, v30, v108, v109
	v_mfma_f32_16x16x32_bf16 v[26:29], v[110:113], v[50:53], v[114:117]
	v_mul_f32_e32 v110, 0x3e000000, v34
	v_mul_f32_e32 v111, 0x3e000000, v35
	v_mul_f32_e32 v112, 0x3e000000, v36
	v_mul_f32_e32 v113, 0x3e000000, v37
	v_max3_f32 v30, v30, v110, v111
	v_mfma_f32_16x16x32_bf16 v[38:41], v[22:25], v[50:53], v[14:17]
	s_nop 1
	v_mul_f32_e32 v114, 0x3e000000, v26
	v_mul_f32_e32 v115, 0x3e000000, v27
	v_mul_f32_e32 v116, 0x3e000000, v28
	v_max3_f32 v14, v30, v112, v113
	s_waitcnt lgkmcnt(1)
	v_mfma_f32_16x16x32_bf16 v[30:33], v[94:97], v[50:53], v[18:21]
	v_lshl_add_u64 v[248:249], v[78:79], 0, 0
	v_lshl_add_u64 v[238:239], v[80:81], 0, 0
	global_load_dwordx4 v[94:97], v[78:79], off
	global_load_dwordx4 v[106:109], v[80:81], off
	global_load_dword v250, v[248:249], off offset:128
	global_load_dword v251, v[238:239], off offset:128
	v_mul_f32_e32 v117, 0x3e000000, v29
	v_max3_f32 v14, v14, v114, v115
	v_max3_f32 v22, v14, v116, v117
	ds_read_b128 v[14:17], v90 offset:6912
	v_mul_f32_e32 v23, 0x3e000000, v38
	v_mul_f32_e32 v24, 0x3e000000, v39
	v_mul_f32_e32 v25, 0x3e000000, v40
	v_mul_f32_e32 v77, 0x3e000000, v41
	v_max3_f32 v22, v22, v23, v24
	s_waitcnt lgkmcnt(1)
	v_mfma_f32_16x16x32_bf16 v[18:21], v[98:101], v[50:53], v[102:105]
	v_mul_f32_e32 v98, 0x3e000000, v30
	v_mul_f32_e32 v99, 0x3e000000, v31
	v_max3_f32 v22, v22, v25, v77
	v_max3_f32 v77, v22, v98, v99
	ds_read_b128 v[22:25], v90 offset:6976
	s_waitcnt vmcnt(5)
	ds_write_b128 v73, v[6:9] offset:18432
	s_waitcnt vmcnt(4)
	ds_write_b128 v73, v[10:13] offset:27648
	s_waitcnt lgkmcnt(0)
	s_barrier
	ds_read_b128 v[6:9], v90 offset:18432
	v_mul_f32_e32 v100, 0x3e000000, v32
	v_mul_f32_e32 v10, 0x3e000000, v33
	v_mfma_f32_16x16x32_bf16 v[14:17], v[14:17], v[2:5], 0
	v_max3_f32 v77, v77, v100, v10
	ds_read_b128 v[10:13], v90 offset:18496
	v_mul_f32_e32 v98, 0x3e000000, v18
	v_mfma_f32_16x16x32_bf16 v[22:25], v[22:25], v[50:53], v[14:17]
	v_mul_f32_e32 v99, 0x3e000000, v21
	ds_read_b128 v[110:113], v90 offset:25408
	s_nop 1
	v_mul_f32_e32 v14, 0x3e000000, v19
	v_max3_f32 v77, v77, v98, v14
	s_waitcnt lgkmcnt(2)
	v_mfma_f32_16x16x32_bf16 v[6:9], v[6:9], v[2:5], 0
	ds_read_b128 v[14:17], v90 offset:20736
	v_mul_f32_e32 v98, 0x3e000000, v20
	v_max3_f32 v77, v77, v98, v99
	s_waitcnt lgkmcnt(2)
	v_mfma_f32_16x16x32_bf16 v[10:13], v[10:13], v[50:53], v[6:9]
	v_mul_f32_e32 v98, 0x3e000000, v22
	v_mul_f32_e32 v99, 0x3e000000, v23
	v_max3_f32 v77, v77, v98, v99
	ds_read_b128 v[6:9], v90 offset:20800
	s_waitcnt lgkmcnt(1)
	v_mfma_f32_16x16x32_bf16 v[14:17], v[14:17], v[2:5], 0
	ds_read_b128 v[98:101], v90 offset:23040
	v_mul_f32_e32 v102, 0x3e000000, v24
	v_mul_f32_e32 v103, 0x3e000000, v25
	s_waitcnt lgkmcnt(1)
	v_mfma_f32_16x16x32_bf16 v[14:17], v[6:9], v[50:53], v[14:17]
	ds_read_b128 v[6:9], v90 offset:23104
	v_max3_f32 v77, v77, v102, v103
	ds_read_b128 v[102:105], v90 offset:25344
	s_waitcnt lgkmcnt(2)
	v_mfma_f32_16x16x32_bf16 v[98:101], v[98:101], v[2:5], 0
	v_mul_f32_e32 v114, 0x3e000000, v10
	v_mul_f32_e32 v115, 0x3e000000, v11
	v_mul_f32_e32 v116, 0x3e000000, v12
	s_waitcnt lgkmcnt(1)
	v_mfma_f32_16x16x32_bf16 v[6:9], v[6:9], v[50:53], v[98:101]
	v_mul_f32_e32 v117, 0x3e000000, v13
	v_max3_f32 v77, v77, v114, v115
	v_mul_f32_e32 v118, 0x3e000000, v14
	v_mul_f32_e32 v119, 0x3e000000, v15
	s_waitcnt lgkmcnt(0)
	v_mfma_f32_16x16x32_bf16 v[2:5], v[102:105], v[2:5], 0
	v_max3_f32 v77, v77, v116, v117
	v_mul_f32_e32 v90, 0x3e000000, v16
	v_mul_f32_e32 v98, 0x3e000000, v17
	v_max3_f32 v77, v77, v118, v119
	v_mul_f32_e32 v99, 0x3e000000, v6
	v_mul_f32_e32 v100, 0x3e000000, v7
	v_max3_f32 v77, v77, v90, v98
	v_mul_f32_e32 v101, 0x3e000000, v8
	v_mul_f32_e32 v102, 0x3e000000, v9
	v_max3_f32 v77, v77, v99, v100
	v_mfma_f32_16x16x32_bf16 v[2:5], v[110:113], v[50:53], v[2:5]
	v_max3_f32 v77, v77, v101, v102
	v_lshl_add_u64 v[248:249], v[78:79], 0, 0
	v_lshl_add_u64 v[238:239], v[80:81], 0, 0
	global_load_dwordx4 v[98:101], v[78:79], off offset:128
	global_load_dwordx4 v[102:105], v[80:81], off offset:128
	global_load_dword v250, v[248:249], off offset:256
	global_load_dword v251, v[238:239], off offset:256
	s_waitcnt vmcnt(7)
	ds_write_b128 v73, v[94:97]
	s_waitcnt vmcnt(6)
	ds_write_b128 v73, v[106:109] offset:9216
	s_nop 0
	v_mul_f32_e32 v50, 0x3e000000, v2
	v_mul_f32_e32 v51, 0x3e000000, v3
	v_mul_f32_e32 v52, 0x3e000000, v4
	v_mul_f32_e32 v53, 0x3e000000, v5
	v_max3_f32 v50, v77, v50, v51
	v_max3_f32 v51, v50, v52, v53
	v_cndmask_b32_e32 v50, v82, v83, vcc
	v_lshlrev_b32_e32 v50, 2, v50
	ds_bpermute_b32 v52, v50, v51
	v_cmp_lt_i32_e32 vcc, v85, v84
	s_waitcnt lgkmcnt(0)
	s_barrier
; #define LAS __attribute__((address_space(3)))
; __device__ __forceinline__ unsigned cvt_pk_bf16(float lo, float hi) { const float __attribute__((ext_vector_type(2))) v = {lo, hi}; return __builtin_bit_cast(unsigned, __builtin_convertvector(v, bf16x2_t)); }
; template <bool LOCAL>
; __device__ __forceinline__ void na_unit(const bf16* P, const bf16* VT, bf16* YCAT, const LAS float* rpb_l, LAS bf16* buf, int b, int gr, int hp, int qblk, int tid) {
;     ...
;             if (sidx == NCH - 1) { m = fmaxf(m, __shfl_xor(m, 16)); m = fmaxf(m, __shfl_xor(m, 32)); }
;         } else {
;             const int c = sidx - NCH;
;             if (LOCAL && c < 8) {
;                 float p[8];
; #pragma unroll
;                 for (int e = 0; e < 4; ++e) { p[e] = __expf(sl[2 * (c < 8 ? c : 0)][e] - m); p[4 + e] = __expf(sl[2 * (c < 8 ? c : 0) + 1][e] - m); }
; #pragma unroll
;                 for (int e = 0; e < 8; ++e) lsum += p[e];
;                 const bf16x8 pf = __builtin_bit_cast(bf16x8, (v4u){pg8::cvt_pk_bf16(p[0], p[1]), pg8::cvt_pk_bf16(p[2], p[3]), pg8::cvt_pk_bf16(p[4], p[5]), pg8::cvt_pk_bf16(p[6], p[7])});
; #pragma unroll
;                 for (int dt = 0; dt < 4; ++dt) { const LAS bf16* vp = cb + (16 * dt + fr) * 72 + kc0 + 4 * fq;
;                     o[dt] = __builtin_amdgcn_mfma_f32_16x16x32_bf16(frag44(vp, vp + 16), pf, o[dt], 0, 0, 0); }
	v_max_f32_e32 v52, v52, v52
	v_max_f32_e32 v52, v51, v52
	v_cndmask_b32_e32 v51, v82, v85, vcc
	v_lshlrev_b32_e32 v51, 2, v51
	ds_bpermute_b32 v53, v51, v52
	s_waitcnt lgkmcnt(0)
	v_max_f32_e32 v53, v53, v53
	v_max_f32_e32 v77, v52, v53
	v_fma_f32 v52, v62, s66, -v77
	v_fma_f32 v64, v64, s66, -v77
	v_mul_f32_e32 v52, 0x3fb8aa3b, v52
	v_fma_f32 v62, v63, s66, -v77
	v_mul_f32_e32 v64, 0x3fb8aa3b, v64
	v_fma_f32 v65, v65, s66, -v77
	v_exp_f32_e32 v53, v52
	v_fma_f32 v52, v66, s66, -v77
	v_mul_f32_e32 v62, 0x3fb8aa3b, v62
	v_exp_f32_e32 v66, v64
	v_fma_f32 v64, v68, s66, -v77
	v_mul_f32_e32 v65, 0x3fb8aa3b, v65
	v_add3_u32 v68, v86, v76, v87
	v_exp_f32_e32 v63, v62
	v_fma_f32 v62, v67, s66, -v77
	v_exp_f32_e32 v67, v65
	v_fma_f32 v65, v69, s66, -v77
	v_add_u32_e32 v69, 0x800, v68
	v_add_u32_e32 v90, 0x1000, v68
	v_add_u32_e32 v134, 0x1800, v68
	ds_read2_b64 v[94:97], v68 offset1:4
	ds_read2_b64 v[110:113], v69 offset0:32 offset1:36
	ds_read2_b64 v[114:117], v90 offset0:64 offset1:68
	ds_read2_b64 v[118:121], v134 offset0:96 offset1:100
	v_mul_f32_e32 v52, 0x3fb8aa3b, v52
	v_mul_f32_e32 v62, 0x3fb8aa3b, v62
	v_mul_f32_e32 v64, 0x3fb8aa3b, v64
	v_mul_f32_e32 v65, 0x3fb8aa3b, v65
	v_exp_f32_e32 v52, v52
	v_exp_f32_e32 v62, v62
	v_exp_f32_e32 v64, v64
	v_exp_f32_e32 v65, v65
	v_cvt_pk_bf16_f32 v106, v53, v63
	v_cvt_pk_bf16_f32 v107, v66, v67
	v_cvt_pk_bf16_f32 v108, v52, v62
	v_cvt_pk_bf16_f32 v109, v64, v65
	v_fma_f32 v58, v58, s66, -v77
	v_fma_f32 v54, v54, s66, -v77
	s_waitcnt lgkmcnt(3)
	v_mfma_f32_16x16x32_bf16 v[94:97], v[94:97], v[106:109], 0
	v_fma_f32 v59, v59, s66, -v77
	v_fma_f32 v55, v55, s66, -v77
	v_fma_f32 v60, v60, s66, -v77
	s_waitcnt lgkmcnt(2)
	v_mfma_f32_16x16x32_bf16 v[110:113], v[110:113], v[106:109], 0
	v_fma_f32 v56, v56, s66, -v77
	v_fma_f32 v61, v61, s66, -v77
	v_fma_f32 v57, v57, s66, -v77
	s_waitcnt lgkmcnt(1)
	v_mfma_f32_16x16x32_bf16 v[114:117], v[114:117], v[106:109], 0
	v_mul_f32_e32 v58, 0x3fb8aa3b, v58
	v_mul_f32_e32 v54, 0x3fb8aa3b, v54
	v_mul_f32_e32 v59, 0x3fb8aa3b, v59
	s_waitcnt lgkmcnt(0)
	v_mfma_f32_16x16x32_bf16 v[106:109], v[118:121], v[106:109], 0
	ds_read2_b64 v[118:121], v68 offset0:8 offset1:12
	v_mul_f32_e32 v55, 0x3fb8aa3b, v55
	v_mul_f32_e32 v60, 0x3fb8aa3b, v60
	v_mul_f32_e32 v56, 0x3fb8aa3b, v56
	v_mul_f32_e32 v61, 0x3fb8aa3b, v61
	v_mul_f32_e32 v57, 0x3fb8aa3b, v57
	v_exp_f32_e32 v58, v58
	v_exp_f32_e32 v54, v54
	v_exp_f32_e32 v59, v59
	v_exp_f32_e32 v55, v55
	v_exp_f32_e32 v60, v60
	v_exp_f32_e32 v56, v56
	v_exp_f32_e32 v61, v61
	v_exp_f32_e32 v57, v57
	v_cvt_pk_bf16_f32 v122, v58, v59
	v_cvt_pk_bf16_f32 v124, v54, v55
	v_cvt_pk_bf16_f32 v123, v60, v61
	v_cvt_pk_bf16_f32 v125, v56, v57
	v_fma_f32 v42, v42, s66, -v77
	v_mul_f32_e32 v42, 0x3fb8aa3b, v42
	s_waitcnt lgkmcnt(0)
	v_mfma_f32_16x16x32_bf16 v[94:97], v[118:121], v[122:125], v[94:97]
	ds_read2_b64 v[118:121], v69 offset0:40 offset1:44
	v_fma_f32 v46, v46, s66, -v77
	v_mul_f32_e32 v46, 0x3fb8aa3b, v46
	s_waitcnt lgkmcnt(0)
	v_mfma_f32_16x16x32_bf16 v[110:113], v[118:121], v[122:125], v[110:113]
	ds_read2_b64 v[118:121], v90 offset0:72 offset1:76
	v_add_u32_e32 v136, 0x5000, v68
	v_fma_f32 v26, v26, s66, -v77
	s_waitcnt lgkmcnt(0)
	v_mfma_f32_16x16x32_bf16 v[114:117], v[118:121], v[122:125], v[114:117]
	ds_read2_b64 v[118:121], v134 offset0:104 offset1:108
	v_lshl_add_u64 v[248:249], v[78:79], 0, 0
	v_lshl_add_u64 v[238:239], v[80:81], 0, 0
	global_load_dwordx4 v[126:129], v[78:79], off offset:256
	global_load_dwordx4 v[130:133], v[80:81], off offset:256
	global_load_dword v250, v[248:249], off offset:384
	global_load_dword v251, v[238:239], off offset:384
	s_waitcnt vmcnt(7)
	ds_write_b128 v73, v[98:101] offset:18432
	s_waitcnt vmcnt(6)
	ds_write_b128 v73, v[102:105] offset:27648
	s_waitcnt lgkmcnt(2)
	v_mfma_f32_16x16x32_bf16 v[106:109], v[118:121], v[122:125], v[106:109]
	v_exp_f32_e32 v119, v42
	v_fma_f32 v42, v47, s66, -v77
	v_mul_f32_e32 v42, 0x3fb8aa3b, v42
	v_exp_f32_e32 v120, v42
	v_fma_f32 v42, v43, s66, -v77
	v_mul_f32_e32 v42, 0x3fb8aa3b, v42
	v_exp_f32_e32 v121, v42
	v_fma_f32 v42, v48, s66, -v77
	v_mul_f32_e32 v42, 0x3fb8aa3b, v42
	v_exp_f32_e32 v122, v42
	v_fma_f32 v42, v44, s66, -v77
	v_mul_f32_e32 v42, 0x3fb8aa3b, v42
	v_add_u32_e32 v124, 0x4800, v68
	s_waitcnt lgkmcnt(0)
	s_barrier
; #define LAS __attribute__((address_space(3)))
; __device__ __forceinline__ unsigned cvt_pk_bf16(float lo, float hi) { const float __attribute__((ext_vector_type(2))) v = {lo, hi}; return __builtin_bit_cast(unsigned, __builtin_convertvector(v, bf16x2_t)); }
; #define NA_STORE(sidx) do { LAS bf16* d_ = buf + ((sidx) & 1) * 9216; _Pragma("unroll") for (int q_ = 0; q_ < 2; ++q_) *(LAS v4u*)(d_ + q_ * 4608 + lrow * 72 + lseg * 8) = ld[(sidx) & 1][q_]; } while (0)
; template <bool LOCAL>
; __device__ __forceinline__ void na_unit(const bf16* P, const bf16* VT, bf16* YCAT, const LAS float* rpb_l, LAS bf16* buf, int b, int gr, int hp, int qblk, int tid) {
;     ...
;             } else {
;                 const int cc = c - NLOC;
; #pragma unroll
;                 for (int p2 = 0; p2 < 2; ++p2) {
;                     float p[8];
; #pragma unroll
;                     for (int e = 0; e < 4; ++e) { p[e] = __expf(sc[4 * (cc >= 0 ? cc : 0) + 2 * p2][e] - m); p[4 + e] = __expf(sc[4 * (cc >= 0 ? cc : 0) + 2 * p2 + 1][e] - m); }
; #pragma unroll
;                     for (int e = 0; e < 8; ++e) lsum += p[e];
;                     const bf16x8 pf = __builtin_bit_cast(bf16x8, (v4u){pg8::cvt_pk_bf16(p[0], p[1]), pg8::cvt_pk_bf16(p[2], p[3]), pg8::cvt_pk_bf16(p[4], p[5]), pg8::cvt_pk_bf16(p[6], p[7])});
; #pragma unroll
;                     for (int dt = 0; dt < 4; ++dt) { const LAS bf16* vp = cb + (16 * dt + fr) * 72 + 32 * p2 + 4 * fq;
;                         o[dt] = __builtin_amdgcn_mfma_f32_16x16x32_bf16(frag44(vp, vp + 16), pf, o[dt], 0, 0, 0); }
;                 }
;             }
;         }
;         if (sidx + 1 < 2 * NCH) NA_STORE(sidx + 1);
;         __syncthreads();
	v_exp_f32_e32 v118, v46
	v_exp_f32_e32 v123, v42
	v_fma_f32 v42, v49, s66, -v77
	ds_read2_b64 v[46:49], v124 offset1:4
	v_mul_f32_e32 v42, 0x3fb8aa3b, v42
	v_exp_f32_e32 v125, v42
	v_fma_f32 v42, v45, s66, -v77
	v_mul_f32_e32 v42, 0x3fb8aa3b, v42
	v_exp_f32_e32 v135, v42
	v_cvt_pk_bf16_f32 v42, v118, v120
	v_cvt_pk_bf16_f32 v43, v122, v125
	v_cvt_pk_bf16_f32 v44, v119, v121
	v_cvt_pk_bf16_f32 v45, v123, v135
	v_mul_f32_e32 v26, 0x3fb8aa3b, v26
	v_fma_f32 v34, v34, s66, -v77
	s_waitcnt lgkmcnt(0)
	v_mfma_f32_16x16x32_bf16 v[46:49], v[46:49], v[42:45], v[94:97]
	v_mul_f32_e32 v34, 0x3fb8aa3b, v34
	v_fma_f32 v30, v30, s66, -v77
	v_mul_f32_e32 v30, 0x3fb8aa3b, v30
	ds_read2_b64 v[94:97], v136 offset0:32 offset1:36
	s_waitcnt lgkmcnt(0)
	v_mfma_f32_16x16x32_bf16 v[94:97], v[94:97], v[42:45], v[110:113]
	s_nop 2
	v_add_u32_e32 v110, 0x5800, v68
	v_add_u32_e32 v111, 0x6000, v68
	ds_read2_b64 v[98:101], v110 offset0:64 offset1:68
	ds_read2_b64 v[102:105], v111 offset0:96 offset1:100
	s_waitcnt lgkmcnt(1)
	v_mfma_f32_16x16x32_bf16 v[98:101], v[98:101], v[42:45], v[114:117]
	v_fma_f32 v38, v38, s66, -v77
	v_mul_f32_e32 v38, 0x3fb8aa3b, v38
	v_fma_f32 v18, v18, s66, -v77
	s_waitcnt lgkmcnt(0)
	v_mfma_f32_16x16x32_bf16 v[42:45], v[102:105], v[42:45], v[106:109]
	v_mul_f32_e32 v18, 0x3fb8aa3b, v18
	v_fma_f32 v10, v10, s66, -v77
	v_mul_f32_e32 v10, 0x3fb8aa3b, v10
	v_exp_f32_e32 v107, v26
	v_fma_f32 v26, v35, s66, -v77
	v_mul_f32_e32 v26, 0x3fb8aa3b, v26
	v_exp_f32_e32 v108, v26
	v_fma_f32 v26, v27, s66, -v77
	v_mul_f32_e32 v26, 0x3fb8aa3b, v26
	v_exp_f32_e32 v109, v26
	v_fma_f32 v26, v36, s66, -v77
	v_mul_f32_e32 v26, 0x3fb8aa3b, v26
	v_exp_f32_e32 v112, v26
	v_fma_f32 v26, v28, s66, -v77
	v_mul_f32_e32 v26, 0x3fb8aa3b, v26
	v_exp_f32_e32 v106, v34
	v_exp_f32_e32 v113, v26
	v_fma_f32 v26, v37, s66, -v77
	ds_read2_b64 v[34:37], v124 offset0:8 offset1:12
	v_mul_f32_e32 v26, 0x3fb8aa3b, v26
	v_exp_f32_e32 v114, v26
	v_fma_f32 v26, v29, s66, -v77
	v_mul_f32_e32 v26, 0x3fb8aa3b, v26
	v_exp_f32_e32 v115, v26
	v_cvt_pk_bf16_f32 v26, v106, v108
	v_cvt_pk_bf16_f32 v27, v112, v114
	v_cvt_pk_bf16_f32 v28, v107, v109
	v_cvt_pk_bf16_f32 v29, v113, v115
	v_fma_f32 v2, v2, s66, -v77
	v_mul_f32_e32 v2, 0x3fb8aa3b, v2
	s_waitcnt lgkmcnt(0)
	v_mfma_f32_16x16x32_bf16 v[34:37], v[34:37], v[26:29], v[46:49]
	v_fma_f32 v6, v6, s66, -v77
	v_mul_f32_e32 v6, 0x3fb8aa3b, v6
	s_nop 0
	ds_read2_b64 v[46:49], v136 offset0:40 offset1:44
	s_waitcnt lgkmcnt(0)
	v_mfma_f32_16x16x32_bf16 v[46:49], v[46:49], v[26:29], v[94:97]
	s_nop 2
	ds_read2_b64 v[94:97], v110 offset0:72 offset1:76
	s_waitcnt lgkmcnt(0)
	v_mfma_f32_16x16x32_bf16 v[94:97], v[94:97], v[26:29], v[98:101]
	s_nop 2
	ds_read2_b64 v[98:101], v111 offset0:104 offset1:108
	global_load_dwordx4 v[102:105], v[78:79], off offset:384
	s_nop 0
	global_load_dwordx4 v[78:81], v[80:81], off offset:384
	s_waitcnt vmcnt(5)
	ds_write_b128 v73, v[126:129]
	s_waitcnt vmcnt(4)
	ds_write_b128 v73, v[130:133] offset:9216
	s_waitcnt lgkmcnt(2)
	v_mfma_f32_16x16x32_bf16 v[26:29], v[98:101], v[26:29], v[42:45]
	v_exp_f32_e32 v99, v30
	v_fma_f32 v30, v39, s66, -v77
	v_mul_f32_e32 v30, 0x3fb8aa3b, v30
	v_exp_f32_e32 v100, v30
	v_fma_f32 v30, v31, s66, -v77
	v_mul_f32_e32 v30, 0x3fb8aa3b, v30
	v_exp_f32_e32 v101, v30
	v_fma_f32 v30, v40, s66, -v77
	v_mul_f32_e32 v30, 0x3fb8aa3b, v30
	v_exp_f32_e32 v116, v30
	v_fma_f32 v30, v32, s66, -v77
	v_mul_f32_e32 v30, 0x3fb8aa3b, v30
	s_waitcnt lgkmcnt(0)
	s_barrier
	v_exp_f32_e32 v98, v38
	v_exp_f32_e32 v117, v30
	v_fma_f32 v30, v41, s66, -v77
	ds_read2_b64 v[38:41], v68 offset1:4
	v_mul_f32_e32 v30, 0x3fb8aa3b, v30
	v_exp_f32_e32 v126, v30
	v_fma_f32 v30, v33, s66, -v77
	v_mul_f32_e32 v30, 0x3fb8aa3b, v30
	v_exp_f32_e32 v127, v30
	v_cvt_pk_bf16_f32 v30, v98, v100
	v_cvt_pk_bf16_f32 v31, v116, v126
	v_cvt_pk_bf16_f32 v32, v99, v101
	v_cvt_pk_bf16_f32 v33, v117, v127
	ds_read2_b64 v[42:45], v90 offset0:64 offset1:68
	s_waitcnt lgkmcnt(1)
	v_mfma_f32_16x16x32_bf16 v[34:37], v[38:41], v[30:33], v[34:37]
	ds_read2_b64 v[38:41], v69 offset0:32 offset1:36
	s_waitcnt lgkmcnt(0)
	v_mfma_f32_16x16x32_bf16 v[38:41], v[38:41], v[30:33], v[46:49]
	s_nop 2
	ds_read2_b64 v[46:49], v134 offset0:96 offset1:100
	s_waitcnt lgkmcnt(0)
	v_mfma_f32_16x16x32_bf16 v[26:29], v[46:49], v[30:33], v[26:29]
	v_exp_f32_e32 v46, v18
	v_fma_f32 v18, v22, s66, -v77
	v_mul_f32_e32 v18, 0x3fb8aa3b, v18
	v_exp_f32_e32 v47, v18
	v_fma_f32 v18, v19, s66, -v77
	v_mul_f32_e32 v18, 0x3fb8aa3b, v18
	v_exp_f32_e32 v48, v18
	v_fma_f32 v18, v23, s66, -v77
	v_mul_f32_e32 v18, 0x3fb8aa3b, v18
	v_exp_f32_e32 v49, v18
	v_fma_f32 v18, v20, s66, -v77
	v_mul_f32_e32 v18, 0x3fb8aa3b, v18
	v_mfma_f32_16x16x32_bf16 v[42:45], v[42:45], v[30:33], v[94:97]
	ds_read2_b64 v[30:33], v69 offset0:40 offset1:44
	s_nop 1
	v_exp_f32_e32 v94, v18
	v_fma_f32 v18, v24, s66, -v77
	v_mul_f32_e32 v18, 0x3fb8aa3b, v18
	v_exp_f32_e32 v95, v18
	v_fma_f32 v18, v21, s66, -v77
	v_mul_f32_e32 v22, 0x3fb8aa3b, v18
	ds_read2_b64 v[18:21], v68 offset0:8 offset1:12
	v_exp_f32_e32 v68, v22
	v_fma_f32 v22, v25, s66, -v77
	v_mul_f32_e32 v22, 0x3fb8aa3b, v22
	v_exp_f32_e32 v96, v22
	v_cvt_pk_bf16_f32 v22, v46, v48
	v_cvt_pk_bf16_f32 v23, v94, v68
	v_cvt_pk_bf16_f32 v24, v47, v49
	v_cvt_pk_bf16_f32 v25, v95, v96
	s_waitcnt lgkmcnt(0)
	s_nop 0
	v_mfma_f32_16x16x32_bf16 v[18:21], v[18:21], v[22:25], v[34:37]
	v_mfma_f32_16x16x32_bf16 v[30:33], v[30:33], v[22:25], v[38:41]
	s_nop 1
	ds_read2_b64 v[34:37], v90 offset0:72 offset1:76
	ds_read2_b64 v[38:41], v134 offset0:104 offset1:108
	s_waitcnt lgkmcnt(1)
	v_mfma_f32_16x16x32_bf16 v[34:37], v[34:37], v[22:25], v[42:45]
	s_waitcnt vmcnt(1)
	ds_write_b128 v73, v[102:105] offset:18432
	s_waitcnt vmcnt(0)
	ds_write_b128 v73, v[78:81] offset:27648
	s_waitcnt lgkmcnt(0)
	s_barrier
; #define LAS __attribute__((address_space(3)))
; __device__ __forceinline__ unsigned cvt_pk_bf16(float lo, float hi) { const float __attribute__((ext_vector_type(2))) v = {lo, hi}; return __builtin_bit_cast(unsigned, __builtin_convertvector(v, bf16x2_t)); }
; #define NA_STORE(sidx) do { LAS bf16* d_ = buf + ((sidx) & 1) * 9216; _Pragma("unroll") for (int q_ = 0; q_ < 2; ++q_) *(LAS v4u*)(d_ + q_ * 4608 + lrow * 72 + lseg * 8) = ld[(sidx) & 1][q_]; } while (0)
; template <bool LOCAL>
; __device__ __forceinline__ void na_unit(const bf16* P, const bf16* VT, bf16* YCAT, const LAS float* rpb_l, LAS bf16* buf, int b, int gr, int hp, int qblk, int tid) {
;     ...
;                 const int cc = c - NLOC;
; #pragma unroll
;                 for (int p2 = 0; p2 < 2; ++p2) {
;                     float p[8];
; #pragma unroll
;                     for (int e = 0; e < 4; ++e) { p[e] = __expf(sc[4 * (cc >= 0 ? cc : 0) + 2 * p2][e] - m); p[4 + e] = __expf(sc[4 * (cc >= 0 ? cc : 0) + 2 * p2 + 1][e] - m); }
; #pragma unroll
;                     for (int e = 0; e < 8; ++e) lsum += p[e];
;                     const bf16x8 pf = __builtin_bit_cast(bf16x8, (v4u){pg8::cvt_pk_bf16(p[0], p[1]), pg8::cvt_pk_bf16(p[2], p[3]), pg8::cvt_pk_bf16(p[4], p[5]), pg8::cvt_pk_bf16(p[6], p[7])});
; #pragma unroll
;                     for (int dt = 0; dt < 4; ++dt) { const LAS bf16* vp = cb + (16 * dt + fr) * 72 + 32 * p2 + 4 * fq;
;                         o[dt] = __builtin_amdgcn_mfma_f32_16x16x32_bf16(frag44(vp, vp + 16), pf, o[dt], 0, 0, 0); }
;                 }
;             }
;         }
;         if (sidx + 1 < 2 * NCH) NA_STORE(sidx + 1);
;         __syncthreads();
;     }
;     ...
;     lsum += __shfl_xor(lsum, 16); lsum += __shfl_xor(lsum, 32);
;     const float inv = 1.f / lsum;
;     bf16* op = YCAT + (size_t)(qrow0 + fr) * D + 512 + h * 64 + 4 * fq;
; #pragma unroll
;     for (int dt = 0; dt < 4; ++dt) { v2u w; w.x = pg8::cvt_pk_bf16(o[dt][0] * inv, o[dt][1] * inv); w.y = pg8::cvt_pk_bf16(o[dt][2] * inv, o[dt][3] * inv); *(v2u*)(op + dt * 16) = w; }
	v_mfma_f32_16x16x32_bf16 v[22:25], v[38:41], v[22:25], v[26:29]
	v_exp_f32_e32 v38, v10
	v_fma_f32 v10, v14, s66, -v77
	v_mul_f32_e32 v10, 0x3fb8aa3b, v10
	v_exp_f32_e32 v39, v10
	v_fma_f32 v10, v11, s66, -v77
	v_mul_f32_e32 v10, 0x3fb8aa3b, v10
	v_exp_f32_e32 v40, v10
	v_fma_f32 v10, v15, s66, -v77
	v_mul_f32_e32 v10, 0x3fb8aa3b, v10
	v_exp_f32_e32 v41, v10
	v_fma_f32 v10, v12, s66, -v77
	v_mul_f32_e32 v10, 0x3fb8aa3b, v10
	v_exp_f32_e32 v42, v10
	v_fma_f32 v10, v16, s66, -v77
	v_mul_f32_e32 v10, 0x3fb8aa3b, v10
	v_exp_f32_e32 v43, v10
	v_fma_f32 v10, v13, s66, -v77
	ds_read2_b64 v[26:29], v110 offset0:64 offset1:68
	v_mul_f32_e32 v14, 0x3fb8aa3b, v10
	v_exp_f32_e32 v44, v14
	v_fma_f32 v14, v17, s66, -v77
	v_mul_f32_e32 v14, 0x3fb8aa3b, v14
	v_exp_f32_e32 v45, v14
	v_cvt_pk_bf16_f32 v14, v38, v40
	v_cvt_pk_bf16_f32 v15, v42, v44
	v_cvt_pk_bf16_f32 v16, v39, v41
	v_cvt_pk_bf16_f32 v17, v43, v45
	ds_read2_b64 v[10:13], v124 offset1:4
	v_mov_b32_e32 v73, v71
	s_waitcnt lgkmcnt(1)
	v_mfma_f32_16x16x32_bf16 v[26:29], v[26:29], v[14:17], v[34:37]
	s_nop 2
	v_add_f32_e32 v34, 0, v53
	v_add_f32_e32 v34, v63, v34
	v_add_f32_e32 v34, v66, v34
	v_add_f32_e32 v34, v67, v34
	v_add_f32_e32 v34, v52, v34
	v_add_f32_e32 v34, v62, v34
	v_add_f32_e32 v34, v64, v34
	v_add_f32_e32 v34, v65, v34
	v_add_f32_e32 v34, v58, v34
	v_add_f32_e32 v34, v59, v34
	v_add_f32_e32 v34, v60, v34
	v_add_f32_e32 v34, v61, v34
	v_add_f32_e32 v34, v54, v34
	v_add_f32_e32 v34, v55, v34
	v_add_f32_e32 v34, v56, v34
	v_add_f32_e32 v34, v57, v34
	s_waitcnt lgkmcnt(0)
	v_mfma_f32_16x16x32_bf16 v[10:13], v[10:13], v[14:17], v[18:21]
	v_add_f32_e32 v34, v118, v34
	v_add_f32_e32 v34, v120, v34
	v_add_f32_e32 v34, v122, v34
	ds_read2_b64 v[18:21], v136 offset0:32 offset1:36
	v_add_f32_e32 v34, v125, v34
	v_add_f32_e32 v34, v119, v34
	v_add_f32_e32 v34, v121, v34
	v_add_f32_e32 v34, v123, v34
	v_add_f32_e32 v34, v135, v34
	v_add_f32_e32 v34, v106, v34
	s_waitcnt lgkmcnt(0)
	v_mfma_f32_16x16x32_bf16 v[18:21], v[18:21], v[14:17], v[30:33]
	v_add_f32_e32 v34, v108, v34
	s_nop 1
	ds_read2_b64 v[30:33], v111 offset0:96 offset1:100
	v_add_f32_e32 v34, v112, v34
	v_add_f32_e32 v34, v114, v34
	v_add_f32_e32 v34, v107, v34
	v_add_f32_e32 v34, v109, v34
	v_add_f32_e32 v34, v113, v34
	v_add_f32_e32 v34, v115, v34
	v_add_f32_e32 v34, v98, v34
	v_add_f32_e32 v34, v100, v34
	s_waitcnt lgkmcnt(0)
	v_mfma_f32_16x16x32_bf16 v[14:17], v[30:33], v[14:17], v[22:25]
	v_add_f32_e32 v34, v116, v34
	v_add_f32_e32 v34, v126, v34
	v_add_f32_e32 v34, v99, v34
	v_exp_f32_e32 v23, v2
	v_fma_f32 v2, v7, s66, -v77
	v_mul_f32_e32 v2, 0x3fb8aa3b, v2
	v_exp_f32_e32 v24, v2
	v_fma_f32 v2, v3, s66, -v77
	v_mul_f32_e32 v2, 0x3fb8aa3b, v2
	v_add_f32_e32 v34, v101, v34
	v_exp_f32_e32 v25, v2
	v_fma_f32 v2, v8, s66, -v77
	v_add_f32_e32 v34, v117, v34
	v_mul_f32_e32 v2, 0x3fb8aa3b, v2
	v_add_f32_e32 v34, v127, v34
	v_exp_f32_e32 v30, v2
	v_fma_f32 v2, v4, s66, -v77
	v_add_f32_e32 v34, v46, v34
	v_mul_f32_e32 v2, 0x3fb8aa3b, v2
	v_add_f32_e32 v34, v48, v34
	v_exp_f32_e32 v22, v6
	v_exp_f32_e32 v31, v2
	v_fma_f32 v2, v9, s66, -v77
	ds_read2_b64 v[6:9], v124 offset0:8 offset1:12
	v_add_f32_e32 v34, v94, v34
	v_mul_f32_e32 v2, 0x3fb8aa3b, v2
	v_add_f32_e32 v34, v68, v34
	v_exp_f32_e32 v32, v2
	v_fma_f32 v2, v5, s66, -v77
	v_add_f32_e32 v34, v47, v34
	v_mul_f32_e32 v2, 0x3fb8aa3b, v2
	v_add_f32_e32 v34, v49, v34
	v_exp_f32_e32 v33, v2
	v_add_f32_e32 v34, v95, v34
	v_add_f32_e32 v34, v96, v34
	v_add_f32_e32 v34, v38, v34
	v_add_f32_e32 v34, v40, v34
	v_cvt_pk_bf16_f32 v2, v22, v24
	v_cvt_pk_bf16_f32 v3, v30, v32
	v_cvt_pk_bf16_f32 v4, v23, v25
	v_cvt_pk_bf16_f32 v5, v31, v33
	v_add_f32_e32 v34, v42, v34
	v_add_f32_e32 v34, v44, v34
	s_waitcnt lgkmcnt(0)
	v_mfma_f32_16x16x32_bf16 v[6:9], v[6:9], v[2:5], v[10:13]
	v_add_f32_e32 v34, v39, v34
	v_add_f32_e32 v34, v41, v34
	v_add_f32_e32 v34, v43, v34
	ds_read2_b64 v[10:13], v136 offset0:40 offset1:44
	v_add_f32_e32 v34, v45, v34
	v_add_f32_e32 v22, v22, v34
	v_add_f32_e32 v22, v24, v22
	v_add_f32_e32 v22, v30, v22
	v_add_f32_e32 v22, v32, v22
	s_waitcnt lgkmcnt(0)
	v_mfma_f32_16x16x32_bf16 v[10:13], v[10:13], v[2:5], v[18:21]
	s_nop 2
	ds_read2_b64 v[18:21], v110 offset0:72 offset1:76
	v_add_f32_e32 v22, v23, v22
	v_add_f32_e32 v22, v25, v22
	v_add_f32_e32 v22, v31, v22
	v_add_f32_e32 v30, v33, v22
	ds_bpermute_b32 v31, v50, v30
	ds_read2_b64 v[22:25], v111 offset0:104 offset1:108
	s_waitcnt lgkmcnt(2)
	v_mfma_f32_16x16x32_bf16 v[18:21], v[18:21], v[2:5], v[26:29]
	v_mov_b32_e32 v77, v71
	s_waitcnt lgkmcnt(1)
	s_nop 0
	v_add_f32_e32 v26, v30, v31
	ds_bpermute_b32 v27, v51, v26
	s_waitcnt lgkmcnt(1)
	v_mfma_f32_16x16x32_bf16 v[14:17], v[22:25], v[2:5], v[14:17]
	s_waitcnt lgkmcnt(0)
	v_add_f32_e32 v2, v26, v27
	v_div_scale_f32 v3, s[0:1], v2, v2, 1.0
	v_rcp_f32_e32 v4, v3
	s_barrier
	s_mov_b64 s[0:1], 0
	v_fma_f32 v5, -v3, v4, 1.0
	v_fmac_f32_e32 v4, v5, v4
	v_div_scale_f32 v5, vcc, 1.0, v2, 1.0
	v_mul_f32_e32 v22, v5, v4
	v_fma_f32 v23, -v3, v22, v5
	v_fmac_f32_e32 v22, v23, v4
	v_fma_f32 v3, -v3, v22, v5
	v_div_fmas_f32 v3, v3, v4, v22
	v_div_fixup_f32 v22, v3, v2, 1.0
	v_lshlrev_b64 v[2:3], 11, v[72:73]
	v_lshl_add_u64 v[2:3], s[10:11], 0, v[2:3]
	v_lshl_add_u64 v[2:3], v[2:3], 0, v[74:75]
	v_pk_mul_f32 v[6:7], v[6:7], v[22:23] op_sel_hi:[1,0]
	v_pk_mul_f32 v[8:9], v[8:9], v[22:23] op_sel_hi:[1,0]
	v_lshl_add_u64 v[4:5], v[2:3], 0, v[76:77]
	v_cvt_pk_bf16_f32 v6, v6, v7
	v_cvt_pk_bf16_f32 v7, v8, v9
	global_store_dwordx2 v[4:5], v[6:7], off offset:1024
	v_pk_mul_f32 v[6:7], v[10:11], v[22:23] op_sel_hi:[1,0]
	v_pk_mul_f32 v[8:9], v[12:13], v[22:23] op_sel_hi:[1,0]
	v_cvt_pk_bf16_f32 v6, v6, v7
	v_cvt_pk_bf16_f32 v7, v8, v9
	global_store_dwordx2 v[4:5], v[6:7], off offset:1056
	v_pk_mul_f32 v[6:7], v[18:19], v[22:23] op_sel_hi:[1,0]
	v_pk_mul_f32 v[8:9], v[20:21], v[22:23] op_sel_hi:[1,0]
	v_cvt_pk_bf16_f32 v6, v6, v7
	v_cvt_pk_bf16_f32 v7, v8, v9
	v_lshl_add_u64 v[2:3], v[4:5], 0, s[12:13]
	global_store_dwordx2 v[4:5], v[6:7], off offset:1088
	v_pk_mul_f32 v[4:5], v[14:15], v[22:23] op_sel_hi:[1,0]
	v_pk_mul_f32 v[6:7], v[16:17], v[22:23] op_sel_hi:[1,0]
	v_cvt_pk_bf16_f32 v4, v4, v5

; #define LAS __attribute__((address_space(3)))
; template <bool LOCAL>
; __device__ __forceinline__ void na_unit(const bf16* P, const bf16* VT, bf16* YCAT, const LAS float* rpb_l, LAS bf16* buf, int b, int gr, int hp, int qblk, int tid) {
;     typedef pg8::bf16x8 bf16x8;
;     constexpr int NCH = LOCAL ? 12 : 4, NLOC = LOCAL ? 8 : 0;
;     const int lane = tid & 63, wv = tid >> 6, fr = lane & 15, fq = lane >> 4, hh = wv >> 2, qb = wv & 3, h = 2 * hp + hh;
;     const int qrow0 = LOCAL ? NCTX + b * SEQ + gr * 64 + 16 * qb : b * CTXL + qblk * 64 + 16 * qb;
;     const int r0 = min(max(gr - 4, 0), 24);
;     const int kc0 = qb == 0 ? 0 : qb == 1 ? 8 : qb == 2 ? 24 : 32;
;     const int qcol = 16 * qb + fr, cs = min(max(qcol - 8, 0), 48);
;     const LAS float* rpb = rpb_l + h * 15 * 31;
;     v4u ld[2][2];
;     const int lrow = (tid >> 3) & 63, lseg = tid & 7;
;     ...
;     bf16x8 qf[2];
; #pragma unroll
;     for (int ks = 0; ks < 2; ++ks) qf[ks] = *(const bf16x8*)(P + (size_t)(qrow0 + fr) * DINP + h * 64 + 32 * ks + 8 * fq);
;     f32x4 sl[16], sc[16];
;     float m = -1.0e30f, lsum = 0.f;
;     f32x4 o[4];
; #pragma unroll
;     for (int dt = 0; dt < 4; ++dt) o[dt] = (f32x4){0.f, 0.f, 0.f, 0.f};
;     NA_ISSUE(0); NA_ISSUE(1); NA_STORE(0);
;     __syncthreads();
; #pragma unroll
;     for (int sidx = 0; sidx < 2 * NCH; ++sidx) {
;         if (sidx + 2 < 2 * NCH) NA_ISSUE(sidx + 2);
;         const LAS bf16* cb = buf + (sidx & 1) * 9216 + hh * 4608;
;         if (sidx < NCH) {
;             const int c = sidx;
;             if (LOCAL && c < 8) {
; #pragma unroll
;                 for (int t2 = 0; t2 < 2; ++t2) {
;                     const LAS bf16* kp = cb + (kc0 + 16 * t2 + fr) * 72 + 8 * fq;
;                     f32x4 acc = {0.f, 0.f, 0.f, 0.f};
;                     acc = __builtin_amdgcn_mfma_f32_16x16x32_bf16(*(const LAS bf16x8*)(kp), qf[0], acc, 0, 0, 0);
;                     acc = __builtin_amdgcn_mfma_f32_16x16x32_bf16(*(const LAS bf16x8*)(kp + 32), qf[1], acc, 0, 0, 0);
;                     const LAS float* rb = rpb + (r0 + c - gr + 7) * 31 + 15 - qcol;
; #pragma unroll
;                     for (int e = 0; e < 4; ++e) { const int kcol = kc0 + 16 * t2 + 4 * fq + e; const bool ok = (kcol >= cs) && (kcol < cs + 16);
;                         const float sv = ok ? acc[e] * 0.125f + rb[ok ? kcol : qcol] : -1.0e30f; acc[e] = sv; m = fmaxf(m, sv); }
.LBB0_3762:
	s_or_b64 exec, exec, s[0:1]
	s_bfe_u32 s19, s72, 0x50002
	v_sub_u32_e64 v3, s19, 4 clamp
	s_ashr_i32 s17, s72, 7
	v_readfirstlane_b32 s0, v3
	s_lshl_b32 s26, s17, 11
	s_min_u32 s20, s0, 24
	s_add_i32 s14, s26, 0x1000
	s_lshl_b32 s15, s20, 6
	s_or_b32 s16, s15, s14
	v_mov_b64_e32 v[18:19], s[8:9]
	v_and_b32_e32 v32, 7, v93
	v_or_b32_e32 v3, s16, v88
	s_and_b32 s18, s72, 3
	v_mad_i64_i32 v[4:5], s[0:1], v3, s57, v[18:19]
	v_lshlrev_b32_e32 v26, 4, v32
	v_mov_b32_e32 v27, v71
	v_lshl_add_u64 v[4:5], v[4:5], 0, v[26:27]
	s_lshl_b32 s2, s18, 8
	v_lshl_add_u64 v[4:5], v[4:5], 0, s[2:3]
	global_load_dwordx4 v[10:13], v[4:5], off offset:1024
	global_load_dwordx4 v[14:17], v[4:5], off offset:1152
	s_lshl_b32 s0, s19, 6
	v_lshl_or_b32 v31, v2, 4, v89
	v_lshl_add_u32 v34, s18, 1, v92
	s_or_b32 s0, s14, s0
	v_mad_u32_u24 v2, v88, s64, 0
	v_lshlrev_b32_e32 v72, 6, v34
	s_add_i32 s50, s26, 0x1040
	v_or_b32_e32 v74, s0, v31
	v_add_u32_e32 v75, v2, v26
	v_ashrrev_i32_e32 v73, 31, v72
	v_or_b32_e32 v4, s50, v88
	v_mad_i64_i32 v[2:3], s[0:1], v74, s57, v[18:19]
	v_add_u32_e32 v4, s15, v4
	v_lshl_add_u64 v[2:3], v[72:73], 1, v[2:3]
	v_mad_i64_i32 v[4:5], s[0:1], v4, s57, v[18:19]
	v_lshl_add_u64 v[2:3], v[2:3], 0, v[70:71]
	v_lshl_add_u64 v[20:21], v[4:5], 0, v[26:27]
	global_load_dwordx4 v[6:9], v[2:3], off
	s_nop 0
	global_load_dwordx4 v[2:5], v[2:3], off offset:64
	s_or_b32 s14, s26, s15
	s_addk_i32 s14, 0x1080
	v_or_b32_e32 v24, s14, v88
	v_mad_i64_i32 v[28:29], s[0:1], v24, s57, v[18:19]
	v_lshl_add_u64 v[26:27], v[28:29], 0, v[26:27]
	v_lshl_add_u64 v[22:23], v[20:21], 0, s[2:3]
	v_lshl_add_u64 v[26:27], v[26:27], 0, s[2:3]
	s_mov_b32 s100, 0x60000
	s_mov_b32 s101, 0
	v_lshl_add_u64 v[248:249], v[22:23], 0, s[100:101]
	global_load_dwordx4 v[18:21], v[22:23], off offset:1024
	s_nop 0
	global_load_dwordx4 v[22:25], v[22:23], off offset:1152
	global_load_dword v250, v[248:249], off offset:1024
	global_load_dword v251, v[248:249], off offset:1152
	v_add_u32_e32 v30, v86, v70
	v_add_u32_e32 v33, v90, v89
	v_mad_u32_u24 v36, v33, s64, v30
	s_sub_i32 s0, s20, s19
	s_mulk_i32 s0, 0x7c
	v_sub_u32_e64 v35, v31, 8 clamp
	v_mul_lo_u32 v34, v34, s68
	s_add_i32 s0, s0, 0
	v_min_u32_e32 v35, 48, v35
	v_lshlrev_b32_e32 v77, 2, v91
	v_add_u32_e32 v34, s0, v34
	v_lshlrev_b32_e32 v31, 2, v31
	v_sub_u32_e32 v31, v34, v31
	v_add_u32_e32 v34, v90, v77
	v_cmp_ge_u32_e32 vcc, v34, v35
	v_mov_b32_e32 v91, 0xf149f2ca
	v_lshl_add_u32 v31, v34, 2, v31
	v_mov_b32_e32 v92, 0xf149f2ca
	s_waitcnt vmcnt(7)
	ds_write_b128 v75, v[10:13]
	s_waitcnt vmcnt(6)
	ds_write_b128 v75, v[14:17] offset:9216
	s_waitcnt lgkmcnt(0)
	s_barrier
	ds_read_b32 v240, v31 offset:37792
	ds_read_b32 v241, v31 offset:37796
	ds_read_b32 v242, v31 offset:37800
	ds_read_b32 v243, v31 offset:37804
	ds_read_b32 v244, v31 offset:37856
	ds_read_b32 v245, v31 offset:37860
	ds_read_b32 v246, v31 offset:37864
	ds_read_b32 v247, v31 offset:37868
	v_lshl_add_u64 v[248:249], v[26:27], 0, s[100:101]
	global_load_dwordx4 v[10:13], v[26:27], off offset:1024
	global_load_dwordx4 v[14:17], v[26:27], off offset:1152
	global_load_dword v250, v[248:249], off offset:1024
	global_load_dword v251, v[248:249], off offset:1152
	ds_read_b128 v[26:29], v36
	ds_read_b128 v[38:41], v36 offset:64
	s_waitcnt vmcnt(9) lgkmcnt(1)
	v_mfma_f32_16x16x32_bf16 v[26:29], v[26:29], v[6:9], 0
	v_add_u32_e32 v36, 16, v35
	v_cmp_lt_u32_e64 s[0:1], v34, v36
	s_and_b64 s[28:29], vcc, s[0:1]
	s_waitcnt vmcnt(8) lgkmcnt(0)
	v_mfma_f32_16x16x32_bf16 v[26:29], v[38:41], v[2:5], v[26:29]
	s_nop 2
	s_waitcnt lgkmcnt(0)
	s_nop 3
	v_fmac_f32_e32 v240, 0x3e000000, v26
	v_cndmask_b32_e64 v92, v92, v240, s[28:29]
	s_nop 4
	v_or_b32_e32 v26, 1, v34
	v_cmp_ge_u32_e32 vcc, v26, v35
	v_cmp_lt_u32_e64 s[0:1], v26, v36
	s_and_b64 s[30:31], vcc, s[0:1]
	s_nop 2
	s_waitcnt lgkmcnt(0)
	v_fmac_f32_e32 v241, 0x3e000000, v27
	v_cndmask_b32_e64 v91, v91, v241, s[30:31]
	v_or_b32_e32 v26, 2, v34
	v_cmp_ge_u32_e32 vcc, v26, v35
	v_cmp_lt_u32_e64 s[0:1], v26, v36
	s_and_b64 s[34:35], vcc, s[0:1]
	v_mov_b32_e32 v93, 0xf149f2ca
	v_mov_b32_e32 v94, 0xf149f2ca
	s_nop 2
	s_waitcnt lgkmcnt(0)
	v_fmac_f32_e32 v242, 0x3e000000, v28
	v_cndmask_b32_e64 v94, v94, v242, s[34:35]
	v_or_b32_e32 v26, 3, v34
	v_cmp_ge_u32_e32 vcc, v26, v35
	v_cmp_lt_u32_e64 s[0:1], v26, v36
	s_and_b64 s[36:37], vcc, s[0:1]
	s_nop 2
	s_waitcnt lgkmcnt(0)
	v_fmac_f32_e32 v243, 0x3e000000, v29
	v_cndmask_b32_e64 v93, v93, v243, s[36:37]
	v_add_u32_e32 v37, 16, v90
	v_add_u32_e32 v34, v37, v89
	v_mad_u32_u24 v38, v34, s64, v30
	ds_read_b128 v[26:29], v38
	ds_read_b128 v[38:41], v38 offset:64
	v_add_u32_e32 v37, v37, v77
	v_cmp_ge_u32_e32 vcc, v37, v35
	v_cmp_lt_u32_e64 s[0:1], v37, v36
	s_waitcnt lgkmcnt(1)
	v_mfma_f32_16x16x32_bf16 v[26:29], v[26:29], v[6:9], 0
	s_and_b64 s[38:39], vcc, s[0:1]
	v_mov_b32_e32 v95, 0xf149f2ca
	v_mov_b32_e32 v96, 0xf149f2ca
	s_waitcnt lgkmcnt(0)
	v_mfma_f32_16x16x32_bf16 v[26:29], v[38:41], v[2:5], v[26:29]
	s_nop 2
	s_waitcnt lgkmcnt(0)
	s_nop 3
	v_fmac_f32_e32 v244, 0x3e000000, v26
	v_cndmask_b32_e64 v96, v96, v244, s[38:39]
	s_nop 4
	v_or_b32_e32 v26, 1, v37
	v_cmp_ge_u32_e32 vcc, v26, v35
	v_cmp_lt_u32_e64 s[0:1], v26, v36
	s_and_b64 s[44:45], vcc, s[0:1]
	s_nop 2
	s_waitcnt lgkmcnt(0)
	v_fmac_f32_e32 v245, 0x3e000000, v27
	v_cndmask_b32_e64 v95, v95, v245, s[44:45]
	v_or_b32_e32 v26, 2, v37
	v_cmp_ge_u32_e32 vcc, v26, v35
	v_cmp_lt_u32_e64 s[0:1], v26, v36
	s_and_b64 s[46:47], vcc, s[0:1]
	v_mov_b32_e32 v99, 0xf149f2ca
	v_mov_b32_e32 v100, 0xf149f2ca
	s_nop 2
	s_waitcnt lgkmcnt(0)
	v_fmac_f32_e32 v246, 0x3e000000, v28
	v_cndmask_b32_e64 v100, v100, v246, s[46:47]
	v_or_b32_e32 v26, 3, v37
	v_cmp_ge_u32_e32 vcc, v26, v35
	v_cmp_lt_u32_e64 s[0:1], v26, v36
	s_and_b64 s[48:49], vcc, s[0:1]
	s_nop 2
	s_waitcnt lgkmcnt(0)
	v_fmac_f32_e32 v247, 0x3e000000, v29
	v_cndmask_b32_e64 v99, v99, v247, s[48:49]
	v_mul_u32_u24_e32 v27, 0x90, v33
	v_lshlrev_b32_e32 v26, 3, v32
	v_add_u32_e32 v32, v30, v27
	s_waitcnt vmcnt(7)
	ds_write_b128 v75, v[18:21] offset:18432
	s_waitcnt vmcnt(6)
	ds_write_b128 v75, v[22:25] offset:27648
	s_waitcnt lgkmcnt(0)
	s_barrier
; #define LAS __attribute__((address_space(3)))
; template <bool LOCAL>
; __device__ __forceinline__ void na_unit(const bf16* P, const bf16* VT, bf16* YCAT, const LAS float* rpb_l, LAS bf16* buf, int b, int gr, int hp, int qblk, int tid) {
;     ...
;         if (sidx < NCH) {
;             const int c = sidx;
;             if (LOCAL && c < 8) {
; #pragma unroll
;                 for (int t2 = 0; t2 < 2; ++t2) {
;                     const LAS bf16* kp = cb + (kc0 + 16 * t2 + fr) * 72 + 8 * fq;
;                     f32x4 acc = {0.f, 0.f, 0.f, 0.f};
;                     acc = __builtin_amdgcn_mfma_f32_16x16x32_bf16(*(const LAS bf16x8*)(kp), qf[0], acc, 0, 0, 0);
;                     acc = __builtin_amdgcn_mfma_f32_16x16x32_bf16(*(const LAS bf16x8*)(kp + 32), qf[1], acc, 0, 0, 0);
;                     const LAS float* rb = rpb + (r0 + c - gr + 7) * 31 + 15 - qcol;
; #pragma unroll
;                     for (int e = 0; e < 4; ++e) { const int kcol = kc0 + 16 * t2 + 4 * fq + e; const bool ok = (kcol >= cs) && (kcol < cs + 16);
;                         const float sv = ok ? acc[e] * 0.125f + rb[ok ? kcol : qcol] : -1.0e30f; acc[e] = sv; m = fmaxf(m, sv); }
;                     sl[2 * (c < 8 ? c : 0) + t2] = acc; }
	ds_read_b32 v240, v31 offset:37916
	ds_read_b32 v241, v31 offset:37920
	ds_read_b32 v242, v31 offset:37924
	ds_read_b32 v243, v31 offset:37928
	ds_read_b32 v244, v31 offset:37980
	ds_read_b32 v245, v31 offset:37984
	ds_read_b32 v246, v31 offset:37988
	ds_read_b32 v247, v31 offset:37992
	ds_read_b128 v[18:21], v32 offset:18432
	s_add_i32 s26, s26, s15
	s_add_i32 s0, s26, 0x10c0
	v_or_b32_e32 v24, s0, v88
	v_mov_b64_e32 v[22:23], s[8:9]
	s_lshl_b32 s1, s18, 7
	v_mad_i64_i32 v[22:23], s[18:19], v24, s57, v[22:23]
	v_lshlrev_b32_e32 v70, 1, v26
	v_lshl_add_u64 v[22:23], v[22:23], 0, v[70:71]
	s_lshl_b32 s2, s1, 1
	v_lshl_add_u64 v[22:23], v[22:23], 0, s[2:3]
	ds_read_b128 v[26:29], v32 offset:18496
	s_waitcnt lgkmcnt(1)
	v_mfma_f32_16x16x32_bf16 v[36:39], v[18:21], v[6:9], 0
	v_lshl_add_u64 v[248:249], v[22:23], 0, s[100:101]
	global_load_dwordx4 v[18:21], v[22:23], off offset:1024
	s_nop 0
	global_load_dwordx4 v[22:25], v[22:23], off offset:1152
	global_load_dword v250, v[248:249], off offset:1024
	global_load_dword v251, v[248:249], off offset:1152
	v_mov_b32_e32 v97, 0xf149f2ca
	v_mov_b32_e32 v98, 0xf149f2ca
	s_waitcnt lgkmcnt(0)
	v_mfma_f32_16x16x32_bf16 v[26:29], v[26:29], v[2:5], v[36:39]
	s_nop 2
	s_waitcnt lgkmcnt(0)
	s_nop 3
	v_fmac_f32_e32 v240, 0x3e000000, v26
	v_cndmask_b32_e64 v98, v98, v240, s[28:29]
	s_nop 2
	s_waitcnt lgkmcnt(0)
	s_nop 0
	v_fmac_f32_e32 v241, 0x3e000000, v27
	v_cndmask_b32_e64 v97, v97, v241, s[30:31]
	v_mov_b32_e32 v101, 0xf149f2ca
	v_mov_b32_e32 v102, 0xf149f2ca
	s_nop 2
	s_waitcnt lgkmcnt(0)
	v_fmac_f32_e32 v242, 0x3e000000, v28
	v_cndmask_b32_e64 v102, v102, v242, s[34:35]
	s_nop 2
	s_waitcnt lgkmcnt(0)
	v_fmac_f32_e32 v243, 0x3e000000, v29
	v_cndmask_b32_e64 v101, v101, v243, s[36:37]
	v_mul_u32_u24_e32 v26, 0x90, v34
	v_add_u32_e32 v33, v30, v26
	ds_read_b128 v[26:29], v33 offset:18432
	ds_read_b128 v[34:37], v33 offset:18496
	v_mov_b32_e32 v104, 0xf149f2ca
	v_mov_b32_e32 v106, 0xf149f2ca
	s_waitcnt lgkmcnt(1)
	v_mfma_f32_16x16x32_bf16 v[26:29], v[26:29], v[6:9], 0
	s_waitcnt lgkmcnt(0)
	v_mfma_f32_16x16x32_bf16 v[26:29], v[34:37], v[2:5], v[26:29]
	s_nop 2
	s_waitcnt lgkmcnt(0)
	s_nop 3
	v_fmac_f32_e32 v244, 0x3e000000, v26
	v_cndmask_b32_e64 v106, v106, v244, s[38:39]
	s_nop 2
	s_waitcnt lgkmcnt(0)
	s_nop 0
	v_fmac_f32_e32 v245, 0x3e000000, v27
	v_cndmask_b32_e64 v104, v104, v245, s[44:45]
	v_mov_b32_e32 v108, 0xf149f2ca
	v_mov_b32_e32 v110, 0xf149f2ca
	s_nop 2
	s_waitcnt lgkmcnt(0)
	v_fmac_f32_e32 v246, 0x3e000000, v28
	v_cndmask_b32_e64 v110, v110, v246, s[46:47]
	s_nop 2
	s_waitcnt lgkmcnt(0)
	v_fmac_f32_e32 v247, 0x3e000000, v29
	v_cndmask_b32_e64 v108, v108, v247, s[48:49]
	s_waitcnt vmcnt(7)
	ds_write_b128 v75, v[10:13]
	s_waitcnt vmcnt(6)
	ds_write_b128 v75, v[14:17] offset:9216
	s_waitcnt lgkmcnt(0)
	s_barrier
	ds_read_b32 v240, v31 offset:38040
	ds_read_b32 v241, v31 offset:38044
	ds_read_b32 v242, v31 offset:38048
	ds_read_b32 v243, v31 offset:38052
	ds_read_b32 v244, v31 offset:38104
	ds_read_b32 v245, v31 offset:38108
	ds_read_b32 v246, v31 offset:38112
	ds_read_b32 v247, v31 offset:38116
	ds_read_b128 v[10:13], v32
	ds_read_b128 v[26:29], v32 offset:64
	s_add_i32 s18, s26, 0x1100
	v_or_b32_e32 v16, s18, v88
	v_mov_b64_e32 v[14:15], s[8:9]
	v_mad_i64_i32 v[14:15], s[20:21], v16, s57, v[14:15]
	v_lshl_add_u64 v[14:15], v[14:15], 0, v[70:71]
	v_lshl_add_u64 v[14:15], v[14:15], 0, s[2:3]
	s_waitcnt lgkmcnt(1)
	v_mfma_f32_16x16x32_bf16 v[34:37], v[10:13], v[6:9], 0
	v_lshl_add_u64 v[248:249], v[14:15], 0, s[100:101]
	global_load_dwordx4 v[10:13], v[14:15], off offset:1024
	s_nop 0
	global_load_dwordx4 v[14:17], v[14:15], off offset:1152
	global_load_dword v250, v[248:249], off offset:1024
	global_load_dword v251, v[248:249], off offset:1152
	v_mov_b32_e32 v103, 0xf149f2ca
	v_mov_b32_e32 v105, 0xf149f2ca
	s_waitcnt lgkmcnt(0)
	v_mfma_f32_16x16x32_bf16 v[26:29], v[26:29], v[2:5], v[34:37]
	s_nop 2
	s_waitcnt lgkmcnt(0)
	s_nop 3
	v_fmac_f32_e32 v240, 0x3e000000, v26
	v_cndmask_b32_e64 v105, v105, v240, s[28:29]
	s_nop 2
	s_waitcnt lgkmcnt(0)
	s_nop 0
	v_fmac_f32_e32 v241, 0x3e000000, v27
	v_cndmask_b32_e64 v103, v103, v241, s[30:31]
	v_mov_b32_e32 v107, 0xf149f2ca
	v_mov_b32_e32 v109, 0xf149f2ca
	s_nop 2
	s_waitcnt lgkmcnt(0)
	v_fmac_f32_e32 v242, 0x3e000000, v28
	v_cndmask_b32_e64 v109, v109, v242, s[34:35]
	s_nop 2
	s_waitcnt lgkmcnt(0)
	v_fmac_f32_e32 v243, 0x3e000000, v29
	v_cndmask_b32_e64 v107, v107, v243, s[36:37]
	ds_read_b128 v[26:29], v33
	ds_read_b128 v[34:37], v33 offset:64
	v_mov_b32_e32 v111, 0xf149f2ca
	v_mov_b32_e32 v114, 0xf149f2ca
	s_waitcnt lgkmcnt(1)
	v_mfma_f32_16x16x32_bf16 v[26:29], v[26:29], v[6:9], 0
	s_waitcnt lgkmcnt(0)
	v_mfma_f32_16x16x32_bf16 v[26:29], v[34:37], v[2:5], v[26:29]
	s_nop 2
	s_waitcnt lgkmcnt(0)
	s_nop 3
	v_fmac_f32_e32 v244, 0x3e000000, v26
	v_cndmask_b32_e64 v114, v114, v244, s[38:39]
	s_nop 2
	s_waitcnt lgkmcnt(0)
	s_nop 0
	v_fmac_f32_e32 v245, 0x3e000000, v27
	v_cndmask_b32_e64 v111, v111, v245, s[44:45]
	v_mov_b32_e32 v113, 0xf149f2ca
	v_mov_b32_e32 v117, 0xf149f2ca
	s_nop 2
	s_waitcnt lgkmcnt(0)
	v_fmac_f32_e32 v246, 0x3e000000, v28
	v_cndmask_b32_e64 v117, v117, v246, s[46:47]
	s_nop 2
	s_waitcnt lgkmcnt(0)
	v_fmac_f32_e32 v247, 0x3e000000, v29
	v_cndmask_b32_e64 v113, v113, v247, s[48:49]
	s_waitcnt vmcnt(7)
	ds_write_b128 v75, v[18:21] offset:18432
	s_waitcnt vmcnt(6)
	ds_write_b128 v75, v[22:25] offset:27648
	s_waitcnt lgkmcnt(0)
	s_barrier
; #define LAS __attribute__((address_space(3)))
; template <bool LOCAL>
; __device__ __forceinline__ void na_unit(const bf16* P, const bf16* VT, bf16* YCAT, const LAS float* rpb_l, LAS bf16* buf, int b, int gr, int hp, int qblk, int tid) {
;     ...
;         if (sidx < NCH) {
;             const int c = sidx;
;             if (LOCAL && c < 8) {
; #pragma unroll
;                 for (int t2 = 0; t2 < 2; ++t2) {
;                     const LAS bf16* kp = cb + (kc0 + 16 * t2 + fr) * 72 + 8 * fq;
;                     f32x4 acc = {0.f, 0.f, 0.f, 0.f};
;                     acc = __builtin_amdgcn_mfma_f32_16x16x32_bf16(*(const LAS bf16x8*)(kp), qf[0], acc, 0, 0, 0);
;                     acc = __builtin_amdgcn_mfma_f32_16x16x32_bf16(*(const LAS bf16x8*)(kp + 32), qf[1], acc, 0, 0, 0);
;                     const LAS float* rb = rpb + (r0 + c - gr + 7) * 31 + 15 - qcol;
; #pragma unroll
;                     for (int e = 0; e < 4; ++e) { const int kcol = kc0 + 16 * t2 + 4 * fq + e; const bool ok = (kcol >= cs) && (kcol < cs + 16);
;                         const float sv = ok ? acc[e] * 0.125f + rb[ok ? kcol : qcol] : -1.0e30f; acc[e] = sv; m = fmaxf(m, sv); }
;                     sl[2 * (c < 8 ? c : 0) + t2] = acc; }
	ds_read_b32 v240, v31 offset:38164
	ds_read_b32 v241, v31 offset:38168
	ds_read_b32 v242, v31 offset:38172
	ds_read_b32 v243, v31 offset:38176
	ds_read_b32 v244, v31 offset:38228
	ds_read_b32 v245, v31 offset:38232
	ds_read_b32 v246, v31 offset:38236
	ds_read_b32 v247, v31 offset:38240
	ds_read_b128 v[18:21], v32 offset:18432
	ds_read_b128 v[26:29], v32 offset:18496
	s_add_i32 s20, s26, 0x1140
	v_or_b32_e32 v24, s20, v88
	v_mov_b64_e32 v[22:23], s[8:9]
	v_mad_i64_i32 v[22:23], s[22:23], v24, s57, v[22:23]
	v_lshl_add_u64 v[22:23], v[22:23], 0, v[70:71]
	v_lshl_add_u64 v[22:23], v[22:23], 0, s[2:3]
	s_waitcnt lgkmcnt(1)
	v_mfma_f32_16x16x32_bf16 v[34:37], v[18:21], v[6:9], 0
	v_lshl_add_u64 v[248:249], v[22:23], 0, s[100:101]
	global_load_dwordx4 v[18:21], v[22:23], off offset:1024
	s_nop 0
	global_load_dwordx4 v[22:25], v[22:23], off offset:1152
	global_load_dword v250, v[248:249], off offset:1024
	global_load_dword v251, v[248:249], off offset:1152
	v_mov_b32_e32 v112, 0xf149f2ca
	v_mov_b32_e32 v115, 0xf149f2ca
	s_waitcnt lgkmcnt(0)
	v_mfma_f32_16x16x32_bf16 v[26:29], v[26:29], v[2:5], v[34:37]
	s_nop 2
	s_waitcnt lgkmcnt(0)
	s_nop 3
	v_fmac_f32_e32 v240, 0x3e000000, v26
	v_cndmask_b32_e64 v115, v115, v240, s[28:29]
	s_nop 2
	s_waitcnt lgkmcnt(0)
	s_nop 0
	v_fmac_f32_e32 v241, 0x3e000000, v27
	v_cndmask_b32_e64 v112, v112, v241, s[30:31]
	v_mov_b32_e32 v116, 0xf149f2ca
	v_mov_b32_e32 v118, 0xf149f2ca
	s_nop 2
	s_waitcnt lgkmcnt(0)
	v_fmac_f32_e32 v242, 0x3e000000, v28
	v_cndmask_b32_e64 v118, v118, v242, s[34:35]
	s_nop 2
	s_waitcnt lgkmcnt(0)
	v_fmac_f32_e32 v243, 0x3e000000, v29
	v_cndmask_b32_e64 v116, v116, v243, s[36:37]
	ds_read_b128 v[26:29], v33 offset:18432
	ds_read_b128 v[34:37], v33 offset:18496
	v_mov_b32_e32 v119, 0xf149f2ca
	v_mov_b32_e32 v122, 0xf149f2ca
	s_waitcnt lgkmcnt(1)
	v_mfma_f32_16x16x32_bf16 v[26:29], v[26:29], v[6:9], 0
	s_waitcnt lgkmcnt(0)
	v_mfma_f32_16x16x32_bf16 v[26:29], v[34:37], v[2:5], v[26:29]
	s_nop 2
	s_waitcnt lgkmcnt(0)
	s_nop 3
	v_fmac_f32_e32 v244, 0x3e000000, v26
	v_cndmask_b32_e64 v122, v122, v244, s[38:39]
	s_nop 2
	s_waitcnt lgkmcnt(0)
	s_nop 0
	v_fmac_f32_e32 v245, 0x3e000000, v27
	v_cndmask_b32_e64 v119, v119, v245, s[44:45]
	v_mov_b32_e32 v121, 0xf149f2ca
	v_mov_b32_e32 v125, 0xf149f2ca
	s_nop 2
	s_waitcnt lgkmcnt(0)
	v_fmac_f32_e32 v246, 0x3e000000, v28
	v_cndmask_b32_e64 v125, v125, v246, s[46:47]
	s_nop 2
	s_waitcnt lgkmcnt(0)
	v_fmac_f32_e32 v247, 0x3e000000, v29
	v_cndmask_b32_e64 v121, v121, v247, s[48:49]
	s_waitcnt vmcnt(7)
	ds_write_b128 v75, v[10:13]
	s_waitcnt vmcnt(6)
	ds_write_b128 v75, v[14:17] offset:9216
	s_waitcnt lgkmcnt(0)
	s_barrier
	ds_read_b32 v240, v31 offset:38288
	ds_read_b32 v241, v31 offset:38292
	ds_read_b32 v242, v31 offset:38296
	ds_read_b32 v243, v31 offset:38300
	ds_read_b32 v244, v31 offset:38352
	ds_read_b32 v245, v31 offset:38356
	ds_read_b32 v246, v31 offset:38360
	ds_read_b32 v247, v31 offset:38364
	ds_read_b128 v[10:13], v32
	ds_read_b128 v[26:29], v32 offset:64
	s_add_i32 s22, s26, 0x1180
	v_or_b32_e32 v16, s22, v88
	v_mov_b64_e32 v[14:15], s[8:9]
	v_mad_i64_i32 v[14:15], s[24:25], v16, s57, v[14:15]
	v_lshl_add_u64 v[14:15], v[14:15], 0, v[70:71]
	v_lshl_add_u64 v[14:15], v[14:15], 0, s[2:3]
	s_waitcnt lgkmcnt(1)
	v_mfma_f32_16x16x32_bf16 v[34:37], v[10:13], v[6:9], 0
	v_lshl_add_u64 v[248:249], v[14:15], 0, s[100:101]
	global_load_dwordx4 v[10:13], v[14:15], off offset:1024
	s_nop 0
	global_load_dwordx4 v[14:17], v[14:15], off offset:1152
	global_load_dword v250, v[248:249], off offset:1024
	global_load_dword v251, v[248:249], off offset:1152
	v_mov_b32_e32 v120, 0xf149f2ca
	v_mov_b32_e32 v123, 0xf149f2ca
	s_waitcnt lgkmcnt(0)
	v_mfma_f32_16x16x32_bf16 v[26:29], v[26:29], v[2:5], v[34:37]
	s_nop 2
	s_waitcnt lgkmcnt(0)
	s_nop 3
	v_fmac_f32_e32 v240, 0x3e000000, v26
	v_cndmask_b32_e64 v123, v123, v240, s[28:29]
	s_nop 2
	s_waitcnt lgkmcnt(0)
	s_nop 0
	v_fmac_f32_e32 v241, 0x3e000000, v27
	v_cndmask_b32_e64 v120, v120, v241, s[30:31]
	v_mov_b32_e32 v124, 0xf149f2ca
	v_mov_b32_e32 v126, 0xf149f2ca
	s_nop 2
	s_waitcnt lgkmcnt(0)
	v_fmac_f32_e32 v242, 0x3e000000, v28
	v_cndmask_b32_e64 v126, v126, v242, s[34:35]
	s_nop 2
	s_waitcnt lgkmcnt(0)
	v_fmac_f32_e32 v243, 0x3e000000, v29
	v_cndmask_b32_e64 v124, v124, v243, s[36:37]
	ds_read_b128 v[26:29], v33
	ds_read_b128 v[34:37], v33 offset:64
	v_mov_b32_e32 v128, 0xf149f2ca
	v_mov_b32_e32 v131, 0xf149f2ca
	s_waitcnt lgkmcnt(1)
	v_mfma_f32_16x16x32_bf16 v[26:29], v[26:29], v[6:9], 0
	s_waitcnt lgkmcnt(0)
	v_mfma_f32_16x16x32_bf16 v[26:29], v[34:37], v[2:5], v[26:29]
	s_nop 2
	s_waitcnt lgkmcnt(0)
	s_nop 3
	v_fmac_f32_e32 v244, 0x3e000000, v26
	v_cndmask_b32_e64 v131, v131, v244, s[38:39]
	s_nop 2
	s_waitcnt lgkmcnt(0)
	s_nop 0
	v_fmac_f32_e32 v245, 0x3e000000, v27
	v_cndmask_b32_e64 v128, v128, v245, s[44:45]
	v_mov_b32_e32 v130, 0xf149f2ca
	v_mov_b32_e32 v135, 0xf149f2ca
	s_nop 2
	s_waitcnt lgkmcnt(0)
	v_fmac_f32_e32 v246, 0x3e000000, v28
	v_cndmask_b32_e64 v135, v135, v246, s[46:47]
	s_nop 2
	s_waitcnt lgkmcnt(0)
	v_fmac_f32_e32 v247, 0x3e000000, v29
	v_cndmask_b32_e64 v130, v130, v247, s[48:49]
	s_waitcnt vmcnt(7)
	ds_write_b128 v75, v[18:21] offset:18432
	s_waitcnt vmcnt(6)
	ds_write_b128 v75, v[22:25] offset:27648
	s_waitcnt lgkmcnt(0)
	s_barrier
; #define LAS __attribute__((address_space(3)))
; template <bool LOCAL>
; __device__ __forceinline__ void na_unit(const bf16* P, const bf16* VT, bf16* YCAT, const LAS float* rpb_l, LAS bf16* buf, int b, int gr, int hp, int qblk, int tid) {
;     ...
;         if (sidx < NCH) {
;             const int c = sidx;
;             if (LOCAL && c < 8) {
; #pragma unroll
;                 for (int t2 = 0; t2 < 2; ++t2) {
;                     const LAS bf16* kp = cb + (kc0 + 16 * t2 + fr) * 72 + 8 * fq;
;                     f32x4 acc = {0.f, 0.f, 0.f, 0.f};
;                     acc = __builtin_amdgcn_mfma_f32_16x16x32_bf16(*(const LAS bf16x8*)(kp), qf[0], acc, 0, 0, 0);
;                     acc = __builtin_amdgcn_mfma_f32_16x16x32_bf16(*(const LAS bf16x8*)(kp + 32), qf[1], acc, 0, 0, 0);
;                     const LAS float* rb = rpb + (r0 + c - gr + 7) * 31 + 15 - qcol;
; #pragma unroll
;                     for (int e = 0; e < 4; ++e) { const int kcol = kc0 + 16 * t2 + 4 * fq + e; const bool ok = (kcol >= cs) && (kcol < cs + 16);
;                         const float sv = ok ? acc[e] * 0.125f + rb[ok ? kcol : qcol] : -1.0e30f; acc[e] = sv; m = fmaxf(m, sv); }
;                     sl[2 * (c < 8 ? c : 0) + t2] = acc; }
	ds_read_b32 v240, v31 offset:38412
	ds_read_b32 v241, v31 offset:38416
	ds_read_b32 v242, v31 offset:38420
	ds_read_b32 v243, v31 offset:38424
	ds_read_b32 v244, v31 offset:38476
	ds_read_b32 v245, v31 offset:38480
	ds_read_b32 v246, v31 offset:38484
	ds_read_b32 v247, v31 offset:38488
	ds_read_b128 v[18:21], v32 offset:18432
	ds_read_b128 v[26:29], v32 offset:18496
	s_add_i32 s24, s26, 0x11c0
	v_or_b32_e32 v24, s24, v88
	v_mov_b64_e32 v[22:23], s[8:9]
	v_mad_i64_i32 v[22:23], s[26:27], v24, s57, v[22:23]
	v_lshl_add_u64 v[22:23], v[22:23], 0, v[70:71]
	v_lshl_add_u64 v[22:23], v[22:23], 0, s[2:3]
	s_waitcnt lgkmcnt(1)
	v_mfma_f32_16x16x32_bf16 v[34:37], v[18:21], v[6:9], 0
	global_load_dwordx4 v[18:21], v[22:23], off offset:1024
	s_nop 0
	global_load_dwordx4 v[22:25], v[22:23], off offset:1152
	v_mov_b32_e32 v129, 0xf149f2ca
	v_mov_b32_e32 v132, 0xf149f2ca
	s_waitcnt lgkmcnt(0)
	v_mfma_f32_16x16x32_bf16 v[26:29], v[26:29], v[2:5], v[34:37]
	s_nop 2
	s_waitcnt lgkmcnt(0)
	s_nop 3
	v_fmac_f32_e32 v240, 0x3e000000, v26
	v_cndmask_b32_e64 v132, v132, v240, s[28:29]
	s_nop 2
	s_waitcnt lgkmcnt(0)
	s_nop 0
	v_fmac_f32_e32 v241, 0x3e000000, v27
	v_cndmask_b32_e64 v129, v129, v241, s[30:31]
	v_mov_b32_e32 v134, 0xf149f2ca
	v_mov_b32_e32 v136, 0xf149f2ca
	s_nop 2
	s_waitcnt lgkmcnt(0)
	v_fmac_f32_e32 v242, 0x3e000000, v28
	v_cndmask_b32_e64 v136, v136, v242, s[34:35]
	s_nop 2
	s_waitcnt lgkmcnt(0)
	v_fmac_f32_e32 v243, 0x3e000000, v29
	v_cndmask_b32_e64 v134, v134, v243, s[36:37]
	ds_read_b128 v[26:29], v33 offset:18432
	ds_read_b128 v[34:37], v33 offset:18496
	v_mov_b32_e32 v137, 0xf149f2ca
	v_mov_b32_e32 v140, 0xf149f2ca
	s_waitcnt lgkmcnt(1)
	v_mfma_f32_16x16x32_bf16 v[26:29], v[26:29], v[6:9], 0
	s_waitcnt lgkmcnt(0)
	v_mfma_f32_16x16x32_bf16 v[26:29], v[34:37], v[2:5], v[26:29]
	s_nop 2
	s_waitcnt lgkmcnt(0)
	s_nop 3
	v_fmac_f32_e32 v244, 0x3e000000, v26
	v_cndmask_b32_e64 v140, v140, v244, s[38:39]
	s_nop 2
	s_waitcnt lgkmcnt(0)
	s_nop 0
	v_fmac_f32_e32 v245, 0x3e000000, v27
	v_cndmask_b32_e64 v137, v137, v245, s[44:45]
	v_mov_b32_e32 v139, 0xf149f2ca
	v_mov_b32_e32 v143, 0xf149f2ca
	s_nop 2
	s_waitcnt lgkmcnt(0)
	v_fmac_f32_e32 v246, 0x3e000000, v28
	v_cndmask_b32_e64 v143, v143, v246, s[46:47]
	s_nop 2
	s_waitcnt lgkmcnt(0)
	v_fmac_f32_e32 v247, 0x3e000000, v29
	v_cndmask_b32_e64 v139, v139, v247, s[48:49]
	s_waitcnt vmcnt(5)
	ds_write_b128 v75, v[10:13]
	s_waitcnt vmcnt(4)
	ds_write_b128 v75, v[14:17] offset:9216
	s_waitcnt lgkmcnt(0)
	s_barrier
	ds_read_b32 v240, v31 offset:38536
	ds_read_b32 v241, v31 offset:38540
	ds_read_b32 v242, v31 offset:38544
	ds_read_b32 v243, v31 offset:38548
	ds_read_b32 v244, v31 offset:38600
	ds_read_b32 v245, v31 offset:38604
	ds_read_b32 v246, v31 offset:38608
	ds_read_b32 v247, v31 offset:38612
	ds_read_b128 v[10:13], v32
	ds_read_b128 v[26:29], v32 offset:64
	s_lshl_b32 s26, s17, 8
	v_or_b32_e32 v34, s26, v88
	v_mov_b64_e32 v[14:15], s[8:9]
	v_mad_i64_i32 v[14:15], s[52:53], v34, s57, v[14:15]
	v_lshl_add_u64 v[14:15], v[14:15], 0, v[70:71]
	v_lshl_add_u64 v[14:15], v[14:15], 0, s[2:3]
	s_waitcnt lgkmcnt(1)
	v_mfma_f32_16x16x32_bf16 v[36:39], v[10:13], v[6:9], 0
	v_lshl_add_u64 v[248:249], v[14:15], 0, s[100:101]
	global_load_dwordx4 v[10:13], v[14:15], off offset:1024
	s_nop 0
	global_load_dwordx4 v[14:17], v[14:15], off offset:1152
	global_load_dword v250, v[248:249], off offset:1024
	global_load_dword v251, v[248:249], off offset:1152
	v_mov_b32_e32 v138, 0xf149f2ca
	v_mov_b32_e32 v141, 0xf149f2ca
	s_waitcnt lgkmcnt(0)
	v_mfma_f32_16x16x32_bf16 v[26:29], v[26:29], v[2:5], v[36:39]
	s_nop 2
	s_waitcnt lgkmcnt(0)
	s_nop 3
	v_fmac_f32_e32 v240, 0x3e000000, v26
	v_cndmask_b32_e64 v141, v141, v240, s[28:29]
	s_nop 2
	s_waitcnt lgkmcnt(0)
	s_nop 0
	v_fmac_f32_e32 v241, 0x3e000000, v27
	v_cndmask_b32_e64 v138, v138, v241, s[30:31]
	v_mov_b32_e32 v142, 0xf149f2ca
	v_mov_b32_e32 v144, 0xf149f2ca
	s_nop 2
	s_waitcnt lgkmcnt(0)
	v_fmac_f32_e32 v242, 0x3e000000, v28
	v_cndmask_b32_e64 v144, v144, v242, s[34:35]
	s_nop 2
	s_waitcnt lgkmcnt(0)
	v_fmac_f32_e32 v243, 0x3e000000, v29
	v_cndmask_b32_e64 v142, v142, v243, s[36:37]
	ds_read_b128 v[26:29], v33
	ds_read_b128 v[36:39], v33 offset:64
	v_mov_b32_e32 v145, 0xf149f2ca
	v_mov_b32_e32 v148, 0xf149f2ca
	s_waitcnt lgkmcnt(1)
	v_mfma_f32_16x16x32_bf16 v[26:29], v[26:29], v[6:9], 0
	s_waitcnt lgkmcnt(0)
	v_mfma_f32_16x16x32_bf16 v[26:29], v[36:39], v[2:5], v[26:29]
	s_nop 2
	s_waitcnt lgkmcnt(0)
	s_nop 3
	v_fmac_f32_e32 v244, 0x3e000000, v26
	v_cndmask_b32_e64 v148, v148, v244, s[38:39]
	s_nop 2
	s_waitcnt lgkmcnt(0)
	s_nop 0
	v_fmac_f32_e32 v245, 0x3e000000, v27
	v_cndmask_b32_e64 v145, v145, v245, s[44:45]
	v_mov_b32_e32 v147, 0xf149f2ca
	v_mov_b32_e32 v151, 0xf149f2ca
	s_nop 2
	s_waitcnt lgkmcnt(0)
	v_fmac_f32_e32 v246, 0x3e000000, v28
	v_cndmask_b32_e64 v151, v151, v246, s[46:47]
	s_nop 2
	s_waitcnt lgkmcnt(0)
	v_fmac_f32_e32 v247, 0x3e000000, v29
	v_cndmask_b32_e64 v147, v147, v247, s[48:49]
	s_waitcnt vmcnt(5)
	ds_write_b128 v75, v[18:21] offset:18432
	s_waitcnt vmcnt(4)
	ds_write_b128 v75, v[22:25] offset:27648
	s_waitcnt lgkmcnt(0)
	s_barrier
; #define LAS __attribute__((address_space(3)))
; template <bool LOCAL>
; __device__ __forceinline__ void na_unit(const bf16* P, const bf16* VT, bf16* YCAT, const LAS float* rpb_l, LAS bf16* buf, int b, int gr, int hp, int qblk, int tid) {
;     ...
;         if (sidx < NCH) {
;             const int c = sidx;
;             if (LOCAL && c < 8) {
; #pragma unroll
;                 for (int t2 = 0; t2 < 2; ++t2) {
;                     const LAS bf16* kp = cb + (kc0 + 16 * t2 + fr) * 72 + 8 * fq;
;                     f32x4 acc = {0.f, 0.f, 0.f, 0.f};
;                     acc = __builtin_amdgcn_mfma_f32_16x16x32_bf16(*(const LAS bf16x8*)(kp), qf[0], acc, 0, 0, 0);
;                     acc = __builtin_amdgcn_mfma_f32_16x16x32_bf16(*(const LAS bf16x8*)(kp + 32), qf[1], acc, 0, 0, 0);
;                     const LAS float* rb = rpb + (r0 + c - gr + 7) * 31 + 15 - qcol;
; #pragma unroll
;                     for (int e = 0; e < 4; ++e) { const int kcol = kc0 + 16 * t2 + 4 * fq + e; const bool ok = (kcol >= cs) && (kcol < cs + 16);
;                         const float sv = ok ? acc[e] * 0.125f + rb[ok ? kcol : qcol] : -1.0e30f; acc[e] = sv; m = fmaxf(m, sv); }
;                     sl[2 * (c < 8 ? c : 0) + t2] = acc; }
;             } else {
;                 const int cc = c - NLOC;
; #pragma unroll
;                 for (int t4 = 0; t4 < 4; ++t4) {
;                     const LAS bf16* kp = cb + (16 * t4 + fr) * 72 + 8 * fq;
;                     f32x4 acc = {0.f, 0.f, 0.f, 0.f};
;                     acc = __builtin_amdgcn_mfma_f32_16x16x32_bf16(*(const LAS bf16x8*)(kp), qf[0], acc, 0, 0, 0);
;                     acc = __builtin_amdgcn_mfma_f32_16x16x32_bf16(*(const LAS bf16x8*)(kp + 32), qf[1], acc, 0, 0, 0);
; #pragma unroll
;                     for (int e = 0; e < 4; ++e) { acc[e] *= 0.125f; m = fmaxf(m, acc[e]); }
;                     sc[4 * (cc >= 0 ? cc : 0) + t4] = acc; }
;             }
;             if (sidx == NCH - 1) { m = fmaxf(m, __shfl_xor(m, 16)); m = fmaxf(m, __shfl_xor(m, 32)); }
	ds_read_b32 v240, v31 offset:38660
	ds_read_b32 v241, v31 offset:38664
	ds_read_b32 v242, v31 offset:38668
	ds_read_b32 v243, v31 offset:38672
	ds_read_b32 v244, v31 offset:38724
	ds_read_b32 v245, v31 offset:38728
	ds_read_b32 v246, v31 offset:38732
	ds_read_b32 v247, v31 offset:38736
	ds_read_b128 v[18:21], v32 offset:18432
	ds_read_b128 v[26:29], v32 offset:18496
	v_or_b32_e32 v24, 64, v34
	v_mov_b64_e32 v[22:23], s[8:9]
	v_mad_i64_i32 v[22:23], s[52:53], v24, s57, v[22:23]
	v_lshl_add_u64 v[22:23], v[22:23], 0, v[70:71]
	v_lshl_add_u64 v[22:23], v[22:23], 0, s[2:3]
	s_waitcnt lgkmcnt(1)
	v_mfma_f32_16x16x32_bf16 v[36:39], v[18:21], v[6:9], 0
	v_lshl_add_u64 v[248:249], v[22:23], 0, s[100:101]
	global_load_dwordx4 v[18:21], v[22:23], off offset:1024
	s_nop 0
	global_load_dwordx4 v[22:25], v[22:23], off offset:1152
	global_load_dword v250, v[248:249], off offset:1024
	global_load_dword v251, v[248:249], off offset:1152
	v_mov_b32_e32 v146, 0xf149f2ca
	v_mov_b32_e32 v149, 0xf149f2ca
	s_waitcnt lgkmcnt(0)
	v_mfma_f32_16x16x32_bf16 v[26:29], v[26:29], v[2:5], v[36:39]
	s_nop 2
	s_waitcnt lgkmcnt(0)
	s_nop 3
	v_fmac_f32_e32 v240, 0x3e000000, v26
	v_cndmask_b32_e64 v149, v149, v240, s[28:29]
	s_nop 2
	s_waitcnt lgkmcnt(0)
	s_nop 0
	v_fmac_f32_e32 v241, 0x3e000000, v27
	v_cndmask_b32_e64 v146, v146, v241, s[30:31]
	v_mov_b32_e32 v150, 0xf149f2ca
	v_mov_b32_e32 v152, 0xf149f2ca
	s_nop 2
	s_waitcnt lgkmcnt(0)
	v_fmac_f32_e32 v242, 0x3e000000, v28
	v_cndmask_b32_e64 v152, v152, v242, s[34:35]
	s_nop 2
	s_waitcnt lgkmcnt(0)
	v_fmac_f32_e32 v243, 0x3e000000, v29
	v_cndmask_b32_e64 v150, v150, v243, s[36:37]
	ds_read_b128 v[26:29], v33 offset:18432
	ds_read_b128 v[36:39], v33 offset:18496
	v_mov_b32_e32 v153, 0xf149f2ca
	v_mov_b32_e32 v155, 0xf149f2ca
	s_waitcnt lgkmcnt(1)
	v_mfma_f32_16x16x32_bf16 v[26:29], v[26:29], v[6:9], 0
	s_waitcnt lgkmcnt(0)
	v_mfma_f32_16x16x32_bf16 v[26:29], v[36:39], v[2:5], v[26:29]
	s_nop 2
	s_waitcnt lgkmcnt(0)
	s_nop 3
	v_fmac_f32_e32 v244, 0x3e000000, v26
	v_cndmask_b32_e64 v155, v155, v244, s[38:39]
	s_nop 2
	s_waitcnt lgkmcnt(0)
	s_nop 0
	v_fmac_f32_e32 v245, 0x3e000000, v27
	v_cndmask_b32_e64 v153, v153, v245, s[44:45]
	v_mov_b32_e32 v154, 0xf149f2ca
	v_mov_b32_e32 v157, 0xf149f2ca
	s_nop 2
	s_waitcnt lgkmcnt(0)
	v_fmac_f32_e32 v246, 0x3e000000, v28
	v_cndmask_b32_e64 v157, v157, v246, s[46:47]
	s_nop 2
	s_waitcnt lgkmcnt(0)
	v_fmac_f32_e32 v247, 0x3e000000, v29
	v_cndmask_b32_e64 v154, v154, v247, s[48:49]
	v_max3_f32 v26, v92, s67, v91
	v_max3_f32 v26, v26, v94, v93
	v_max3_f32 v26, v26, v96, v95
	v_max3_f32 v26, v26, v100, v99
	v_max3_f32 v26, v26, v98, v97
	v_max3_f32 v26, v26, v102, v101
	v_max3_f32 v26, v26, v106, v104
	v_max3_f32 v26, v26, v110, v108
	v_max3_f32 v26, v26, v105, v103
	v_max3_f32 v26, v26, v109, v107
	v_max3_f32 v26, v26, v114, v111
	v_max3_f32 v26, v26, v117, v113
	v_max3_f32 v26, v26, v115, v112
	v_max3_f32 v26, v26, v118, v116
	v_max3_f32 v26, v26, v122, v119
	v_max3_f32 v26, v26, v125, v121
	v_max3_f32 v26, v26, v123, v120
	v_max3_f32 v26, v26, v126, v124
	v_max3_f32 v26, v26, v131, v128
	v_max3_f32 v26, v26, v135, v130
	v_max3_f32 v26, v26, v132, v129
	v_max3_f32 v26, v26, v136, v134
	v_max3_f32 v26, v26, v140, v137
	v_max3_f32 v26, v26, v143, v139
	v_max3_f32 v26, v26, v141, v138
	v_max3_f32 v26, v26, v144, v142
	v_mad_u32_u24 v89, v89, s64, v30
	v_max3_f32 v26, v26, v148, v145
	s_waitcnt vmcnt(7)
	ds_write_b128 v75, v[10:13]
	s_waitcnt vmcnt(6)
	ds_write_b128 v75, v[14:17] offset:9216
	s_waitcnt lgkmcnt(0)
	s_barrier
	ds_read_b128 v[10:13], v89
	ds_read_b128 v[14:17], v89 offset:64
	v_max3_f32 v26, v26, v151, v147
	v_max3_f32 v26, v26, v149, v146
	v_max3_f32 v26, v26, v152, v150
	v_max3_f32 v26, v26, v155, v153
	v_max3_f32 v35, v26, v157, v154
	v_or_b32_e32 v26, 0x80, v34
	v_mov_b64_e32 v[44:45], s[8:9]
	v_mad_i64_i32 v[26:27], s[28:29], v26, s57, v[44:45]
	v_lshl_add_u64 v[26:27], v[26:27], 0, v[70:71]
	v_lshl_add_u64 v[30:31], v[26:27], 0, s[2:3]
	s_waitcnt lgkmcnt(1)
	v_mfma_f32_16x16x32_bf16 v[10:13], v[10:13], v[6:9], 0
	v_lshl_add_u64 v[248:249], v[30:31], 0, s[100:101]
	global_load_dwordx4 v[26:29], v[30:31], off offset:1024
	s_nop 0
	global_load_dwordx4 v[30:33], v[30:31], off offset:1152
	global_load_dword v250, v[248:249], off offset:1024
	global_load_dword v251, v[248:249], off offset:1152
	ds_read_b128 v[36:39], v89 offset:2304
	v_lshl_add_u64 v[78:79], s[4:5], 0, v[70:71]
	s_waitcnt lgkmcnt(1)
	v_mfma_f32_16x16x32_bf16 v[62:65], v[14:17], v[2:5], v[10:13]
	s_ashr_i32 s17, s16, 31
	v_mov_b32_e32 v81, v71
	v_cmp_lt_i32_e32 vcc, v83, v84
	ds_read_b128 v[10:13], v89 offset:2368
	v_add3_u32 v156, v86, v76, v87
	s_nop 2
	v_mul_f32_e32 v14, 0x3e000000, v62
	v_mul_f32_e32 v15, 0x3e000000, v63
	v_max3_f32 v35, v35, v14, v15
	v_mul_f32_e32 v40, 0x3e000000, v64
	s_waitcnt lgkmcnt(1)
	v_mfma_f32_16x16x32_bf16 v[14:17], v[36:39], v[6:9], 0
	v_mul_f32_e32 v36, 0x3e000000, v65
	v_max3_f32 v35, v35, v40, v36
	ds_read_b128 v[36:39], v89 offset:4608
	s_waitcnt lgkmcnt(1)
	v_mfma_f32_16x16x32_bf16 v[66:69], v[10:13], v[2:5], v[14:17]
	ds_read_b128 v[10:13], v89 offset:4672
	s_ashr_i32 s19, s18, 31
	s_ashr_i32 s21, s20, 31
	s_ashr_i32 s23, s22, 31
	s_ashr_i32 s25, s24, 31
	s_nop 2
	v_mul_f32_e32 v14, 0x3e000000, v66
	v_mul_f32_e32 v15, 0x3e000000, v67
	v_max3_f32 v35, v35, v14, v15
	s_waitcnt lgkmcnt(1)
	v_mfma_f32_16x16x32_bf16 v[14:17], v[36:39], v[6:9], 0
	v_mul_f32_e32 v40, 0x3e000000, v68
	v_mul_f32_e32 v41, 0x3e000000, v69
	v_max3_f32 v35, v35, v40, v41
	s_waitcnt lgkmcnt(0)
	v_mfma_f32_16x16x32_bf16 v[58:61], v[10:13], v[2:5], v[14:17]
	ds_read_b128 v[36:39], v89 offset:6912
	ds_read_b128 v[40:43], v89 offset:6976
	s_waitcnt vmcnt(7)
	ds_write_b128 v75, v[18:21] offset:18432
	s_waitcnt vmcnt(6)
	ds_write_b128 v75, v[22:25] offset:27648
	s_waitcnt lgkmcnt(0)
	s_nop 0
	v_mul_f32_e32 v10, 0x3e000000, v58
	v_mul_f32_e32 v11, 0x3e000000, v59
	v_max3_f32 v14, v35, v10, v11
	v_mfma_f32_16x16x32_bf16 v[10:13], v[36:39], v[6:9], 0
	v_mul_f32_e32 v15, 0x3e000000, v60
	v_mul_f32_e32 v16, 0x3e000000, v61
	v_max3_f32 v14, v14, v15, v16
	v_mfma_f32_16x16x32_bf16 v[54:57], v[40:43], v[2:5], v[10:13]
	s_barrier
; #define LAS __attribute__((address_space(3)))
; template <bool LOCAL>
; __device__ __forceinline__ void na_unit(const bf16* P, const bf16* VT, bf16* YCAT, const LAS float* rpb_l, LAS bf16* buf, int b, int gr, int hp, int qblk, int tid) {
;     ...
;             } else {
;                 const int cc = c - NLOC;
; #pragma unroll
;                 for (int t4 = 0; t4 < 4; ++t4) {
;                     const LAS bf16* kp = cb + (16 * t4 + fr) * 72 + 8 * fq;
;                     f32x4 acc = {0.f, 0.f, 0.f, 0.f};
;                     acc = __builtin_amdgcn_mfma_f32_16x16x32_bf16(*(const LAS bf16x8*)(kp), qf[0], acc, 0, 0, 0);
;                     acc = __builtin_amdgcn_mfma_f32_16x16x32_bf16(*(const LAS bf16x8*)(kp + 32), qf[1], acc, 0, 0, 0);
; #pragma unroll
;                     for (int e = 0; e < 4; ++e) { acc[e] *= 0.125f; m = fmaxf(m, acc[e]); }
;                     sc[4 * (cc >= 0 ? cc : 0) + t4] = acc; }
;             }
;             if (sidx == NCH - 1) { m = fmaxf(m, __shfl_xor(m, 16)); m = fmaxf(m, __shfl_xor(m, 32)); }
	v_or_b32_e32 v18, 0xc0, v34
	v_mad_i64_i32 v[18:19], s[28:29], v18, s57, v[44:45]
	v_lshl_add_u64 v[18:19], v[18:19], 0, v[70:71]
	s_nop 3
	v_mul_f32_e32 v10, 0x3e000000, v54
	v_mul_f32_e32 v11, 0x3e000000, v55
	v_max3_f32 v14, v14, v10, v11
	ds_read_b128 v[10:13], v89 offset:18432
	v_mul_f32_e32 v15, 0x3e000000, v56
	v_mul_f32_e32 v16, 0x3e000000, v57
	v_max3_f32 v35, v14, v15, v16
	ds_read_b128 v[14:17], v89 offset:18496
	v_lshl_add_u64 v[22:23], v[18:19], 0, s[2:3]
	s_waitcnt lgkmcnt(1)
	v_mfma_f32_16x16x32_bf16 v[10:13], v[10:13], v[6:9], 0
	global_load_dwordx4 v[18:21], v[22:23], off offset:1024
	global_load_dwordx4 v[158:161], v[22:23], off offset:1152
	ds_read_b128 v[22:25], v89 offset:20736
	s_ashr_i32 s27, s26, 31
	s_waitcnt lgkmcnt(1)
	v_mfma_f32_16x16x32_bf16 v[46:49], v[14:17], v[2:5], v[10:13]
	s_nop 2
	ds_read_b128 v[10:13], v89 offset:20800
	s_nop 3
	v_mul_f32_e32 v14, 0x3e000000, v46
	v_mul_f32_e32 v15, 0x3e000000, v47
	v_max3_f32 v34, v35, v14, v15
	v_mul_f32_e32 v35, 0x3e000000, v48
	s_waitcnt lgkmcnt(1)
	v_mfma_f32_16x16x32_bf16 v[14:17], v[22:25], v[6:9], 0
	v_mul_f32_e32 v22, 0x3e000000, v49
	v_max3_f32 v34, v34, v35, v22
	ds_read_b128 v[22:25], v89 offset:23040
	s_waitcnt lgkmcnt(1)
	v_mfma_f32_16x16x32_bf16 v[50:53], v[10:13], v[2:5], v[14:17]
	ds_read_b128 v[10:13], v89 offset:23104
	s_nop 6
	v_mul_f32_e32 v14, 0x3e000000, v50
	v_mul_f32_e32 v15, 0x3e000000, v51
	v_max3_f32 v34, v34, v14, v15
	s_waitcnt lgkmcnt(1)
	v_mfma_f32_16x16x32_bf16 v[14:17], v[22:25], v[6:9], 0
	v_mul_f32_e32 v35, 0x3e000000, v52
	v_mul_f32_e32 v36, 0x3e000000, v53
	v_max3_f32 v38, v34, v35, v36
	s_waitcnt lgkmcnt(0)
	v_mfma_f32_16x16x32_bf16 v[42:45], v[10:13], v[2:5], v[14:17]
	ds_read_b128 v[22:25], v89 offset:25344
	ds_read_b128 v[34:37], v89 offset:25408
	s_waitcnt vmcnt(5)
	ds_write_b128 v75, v[26:29]
	s_waitcnt vmcnt(4)
	ds_write_b128 v75, v[30:33] offset:9216
	s_waitcnt lgkmcnt(0)
	s_nop 0
	v_mul_f32_e32 v10, 0x3e000000, v42
	v_mul_f32_e32 v11, 0x3e000000, v43
	v_max3_f32 v14, v38, v10, v11
	v_mfma_f32_16x16x32_bf16 v[10:13], v[22:25], v[6:9], 0
	v_mul_f32_e32 v15, 0x3e000000, v44
	v_mul_f32_e32 v16, 0x3e000000, v45
	v_max3_f32 v14, v14, v15, v16
	v_mfma_f32_16x16x32_bf16 v[38:41], v[34:37], v[2:5], v[10:13]
	s_barrier
	v_add3_u32 v26, v88, s1, 64
	v_mul_u32_u24_e32 v26, 0x9000, v26
	v_lshl_add_u64 v[22:23], s[16:17], 1, v[78:79]
	s_nop 3
	v_mul_f32_e32 v10, 0x3e000000, v38
	v_mul_f32_e32 v11, 0x3e000000, v39
	v_max3_f32 v10, v14, v10, v11
	v_mul_f32_e32 v11, 0x3e000000, v40
	v_mul_f32_e32 v12, 0x3e000000, v41
	v_max3_f32 v34, v10, v11, v12
	v_or_b32_e32 v10, s1, v88
	v_mul_u32_u24_e32 v14, 0x9000, v10
	ds_read_b128 v[10:13], v89
	v_lshlrev_b32_e32 v70, 1, v14
	ds_read_b128 v[14:17], v89 offset:64
	v_lshlrev_b32_e32 v80, 1, v26
	v_lshl_add_u64 v[24:25], v[22:23], 0, v[70:71]
	v_lshl_add_u64 v[22:23], v[22:23], 0, v[80:81]
	s_waitcnt lgkmcnt(1)
	v_mfma_f32_16x16x32_bf16 v[10:13], v[10:13], v[6:9], 0
	v_lshl_add_u64 v[248:249], v[24:25], 0, 0
	v_lshl_add_u64 v[238:239], v[22:23], 0, 0
	global_load_dwordx4 v[162:165], v[24:25], off
	global_load_dwordx4 v[166:169], v[22:23], off
	global_load_dword v250, v[248:249], off offset:128
	global_load_dword v251, v[238:239], off offset:128
	ds_read_b128 v[22:25], v89 offset:2304
	s_add_i32 s16, s15, s50
	s_waitcnt lgkmcnt(1)
	v_mfma_f32_16x16x32_bf16 v[30:33], v[14:17], v[2:5], v[10:13]
	s_ashr_i32 s17, s16, 31
	s_ashr_i32 s15, s14, 31
	v_lshl_add_u64 v[86:87], s[14:15], 1, v[78:79]
	ds_read_b128 v[10:13], v89 offset:2368
	s_ashr_i32 s1, s0, 31
	s_nop 2
	v_mul_f32_e32 v14, 0x3e000000, v30
	v_mul_f32_e32 v15, 0x3e000000, v31
	v_max3_f32 v26, v34, v14, v15
	v_mul_f32_e32 v27, 0x3e000000, v32
	s_waitcnt lgkmcnt(1)
	v_mfma_f32_16x16x32_bf16 v[14:17], v[22:25], v[6:9], 0
	v_mul_f32_e32 v22, 0x3e000000, v33
	v_max3_f32 v26, v26, v27, v22
	ds_read_b128 v[22:25], v89 offset:4608
	s_waitcnt lgkmcnt(1)
	v_mfma_f32_16x16x32_bf16 v[34:37], v[10:13], v[2:5], v[14:17]
	ds_read_b128 v[10:13], v89 offset:4672
	s_nop 6
	v_mul_f32_e32 v14, 0x3e000000, v34
	v_mul_f32_e32 v15, 0x3e000000, v35
	v_max3_f32 v26, v26, v14, v15
	s_waitcnt lgkmcnt(1)
	v_mfma_f32_16x16x32_bf16 v[14:17], v[22:25], v[6:9], 0
	v_mul_f32_e32 v27, 0x3e000000, v36
	v_mul_f32_e32 v28, 0x3e000000, v37
	v_max3_f32 v88, v26, v27, v28
	s_waitcnt lgkmcnt(0)
	v_mfma_f32_16x16x32_bf16 v[26:29], v[10:13], v[2:5], v[14:17]
	ds_read_b128 v[22:25], v89 offset:6912
	ds_read_b128 v[170:173], v89 offset:6976
	s_waitcnt vmcnt(5)
	ds_write_b128 v75, v[18:21] offset:18432
	s_waitcnt vmcnt(4)
	ds_write_b128 v75, v[158:161] offset:27648
	s_waitcnt lgkmcnt(0)
	s_nop 0
	v_mul_f32_e32 v10, 0x3e000000, v26
	v_mul_f32_e32 v11, 0x3e000000, v27
	v_max3_f32 v14, v88, v10, v11
	v_mfma_f32_16x16x32_bf16 v[10:13], v[22:25], v[6:9], 0
	v_mul_f32_e32 v15, 0x3e000000, v28
	v_mul_f32_e32 v16, 0x3e000000, v29
	v_max3_f32 v14, v14, v15, v16
	v_mfma_f32_16x16x32_bf16 v[22:25], v[170:173], v[2:5], v[10:13]
	s_barrier
; #define LAS __attribute__((address_space(3)))
; __device__ __forceinline__ unsigned cvt_pk_bf16(float lo, float hi) { const float __attribute__((ext_vector_type(2))) v = {lo, hi}; return __builtin_bit_cast(unsigned, __builtin_convertvector(v, bf16x2_t)); }
; template <bool LOCAL>
; __device__ __forceinline__ void na_unit(const bf16* P, const bf16* VT, bf16* YCAT, const LAS float* rpb_l, LAS bf16* buf, int b, int gr, int hp, int qblk, int tid) {
;     ...
;             if (sidx == NCH - 1) { m = fmaxf(m, __shfl_xor(m, 16)); m = fmaxf(m, __shfl_xor(m, 32)); }
;         } else {
;             const int c = sidx - NCH;
;             if (LOCAL && c < 8) {
;                 float p[8];
; #pragma unroll
;                 for (int e = 0; e < 4; ++e) { p[e] = __expf(sl[2 * (c < 8 ? c : 0)][e] - m); p[4 + e] = __expf(sl[2 * (c < 8 ? c : 0) + 1][e] - m); }
; #pragma unroll
;                 for (int e = 0; e < 8; ++e) lsum += p[e];
;                 const bf16x8 pf = __builtin_bit_cast(bf16x8, (v4u){pg8::cvt_pk_bf16(p[0], p[1]), pg8::cvt_pk_bf16(p[2], p[3]), pg8::cvt_pk_bf16(p[4], p[5]), pg8::cvt_pk_bf16(p[6], p[7])});
; #pragma unroll
;                 for (int dt = 0; dt < 4; ++dt) { const LAS bf16* vp = cb + (16 * dt + fr) * 72 + kc0 + 4 * fq;
;                     o[dt] = __builtin_amdgcn_mfma_f32_16x16x32_bf16(frag44(vp, vp + 16), pf, o[dt], 0, 0, 0); }
	v_lshl_add_u64 v[18:19], s[16:17], 1, v[78:79]
	v_lshl_add_u64 v[20:21], v[18:19], 0, v[70:71]
	v_lshl_add_u64 v[18:19], v[18:19], 0, v[80:81]
	s_nop 3
	v_mul_f32_e32 v10, 0x3e000000, v22
	v_mul_f32_e32 v11, 0x3e000000, v23
	v_max3_f32 v14, v14, v10, v11
	ds_read_b128 v[10:13], v89 offset:18432
	v_mul_f32_e32 v15, 0x3e000000, v24
	v_mul_f32_e32 v16, 0x3e000000, v25
	v_max3_f32 v88, v14, v15, v16
	ds_read_b128 v[14:17], v89 offset:18496
	s_waitcnt lgkmcnt(1)
	v_mfma_f32_16x16x32_bf16 v[10:13], v[10:13], v[6:9], 0
	v_lshl_add_u64 v[248:249], v[20:21], 0, 0
	v_lshl_add_u64 v[238:239], v[18:19], 0, 0
	global_load_dwordx4 v[170:173], v[20:21], off
	global_load_dwordx4 v[174:177], v[18:19], off
	global_load_dword v250, v[248:249], off offset:128
	global_load_dword v251, v[238:239], off offset:128
	ds_read_b128 v[18:21], v89 offset:20736
	ds_read_b128 v[158:161], v89 offset:23040
	s_waitcnt lgkmcnt(2)
	v_mfma_f32_16x16x32_bf16 v[14:17], v[14:17], v[2:5], v[10:13]
	s_nop 2
	ds_read_b128 v[10:13], v89 offset:20800
	s_waitcnt lgkmcnt(2)
	v_mfma_f32_16x16x32_bf16 v[18:21], v[18:21], v[6:9], 0
	s_nop 1
	v_mul_f32_e32 v127, 0x3e000000, v14
	v_mul_f32_e32 v133, 0x3e000000, v15
	v_max3_f32 v88, v88, v127, v133
	s_waitcnt lgkmcnt(0)
	v_mfma_f32_16x16x32_bf16 v[18:21], v[10:13], v[2:5], v[18:21]
	ds_read_b128 v[10:13], v89 offset:23104
	ds_read_b128 v[178:181], v89 offset:25344
	ds_read_b128 v[182:185], v89 offset:25408
	v_mul_f32_e32 v127, 0x3e000000, v16
	v_mfma_f32_16x16x32_bf16 v[158:161], v[158:161], v[6:9], 0
	v_mul_f32_e32 v133, 0x3e000000, v17
	v_max3_f32 v88, v88, v127, v133
	s_nop 0
	v_mul_f32_e32 v127, 0x3e000000, v18
	s_waitcnt lgkmcnt(1)
	v_mfma_f32_16x16x32_bf16 v[6:9], v[178:181], v[6:9], 0
	v_mul_f32_e32 v133, 0x3e000000, v19
	v_max3_f32 v88, v88, v127, v133
	v_mul_f32_e32 v127, 0x3e000000, v20
	v_mfma_f32_16x16x32_bf16 v[10:13], v[10:13], v[2:5], v[158:161]
	v_mul_f32_e32 v133, 0x3e000000, v21
	v_max3_f32 v88, v88, v127, v133
	s_waitcnt vmcnt(7)
	ds_write_b128 v75, v[162:165]
	s_waitcnt vmcnt(6)
	ds_write_b128 v75, v[166:169] offset:9216
	s_waitcnt lgkmcnt(2)
	v_mfma_f32_16x16x32_bf16 v[2:5], v[182:185], v[2:5], v[6:9]
	v_mul_f32_e32 v89, 0x3e000000, v10
	v_mul_f32_e32 v127, 0x3e000000, v11
	v_max3_f32 v88, v88, v89, v127
	v_mul_f32_e32 v89, 0x3e000000, v12
	v_mul_f32_e32 v127, 0x3e000000, v13
	v_max3_f32 v88, v88, v89, v127
	s_nop 1
	v_mul_f32_e32 v6, 0x3e000000, v2
	v_mul_f32_e32 v7, 0x3e000000, v3
	v_max3_f32 v6, v88, v6, v7
	v_mul_f32_e32 v7, 0x3e000000, v4
	v_mul_f32_e32 v8, 0x3e000000, v5
	v_max3_f32 v6, v6, v7, v8
	v_cndmask_b32_e32 v7, v82, v83, vcc
	v_lshlrev_b32_e32 v88, 2, v7
	ds_bpermute_b32 v7, v88, v6
	v_cmp_lt_i32_e32 vcc, v85, v84
	v_lshl_add_u32 v8, v90, 1, v156
	s_waitcnt lgkmcnt(0)
	s_barrier
	v_max_f32_e32 v7, v7, v7
	v_max_f32_e32 v6, v6, v7
	v_cndmask_b32_e32 v7, v82, v85, vcc
	v_lshlrev_b32_e32 v89, 2, v7
	ds_bpermute_b32 v7, v89, v6
	s_waitcnt lgkmcnt(0)
	ds_read2_b64 v[158:161], v8 offset1:4
	v_max_f32_e32 v7, v7, v7
	v_max_f32_e32 v133, v6, v7
	v_sub_f32_e32 v6, v92, v133
	v_mul_f32_e32 v6, 0x3fb8aa3b, v6
	v_exp_f32_e32 v127, v6
	v_sub_f32_e32 v6, v96, v133
	v_mul_f32_e32 v6, 0x3fb8aa3b, v6
	v_exp_f32_e32 v92, v6
	v_sub_f32_e32 v6, v91, v133
	v_mul_f32_e32 v6, 0x3fb8aa3b, v6
	v_exp_f32_e32 v96, v6
	v_sub_f32_e32 v6, v95, v133
	v_mul_f32_e32 v6, 0x3fb8aa3b, v6
	v_exp_f32_e32 v91, v6
	v_sub_f32_e32 v6, v94, v133
	v_mul_f32_e32 v6, 0x3fb8aa3b, v6
	v_exp_f32_e32 v95, v6
	v_sub_f32_e32 v6, v100, v133
	v_mul_f32_e32 v6, 0x3fb8aa3b, v6
	v_exp_f32_e32 v94, v6
	v_sub_f32_e32 v6, v93, v133
	v_mul_f32_e32 v6, 0x3fb8aa3b, v6
	v_exp_f32_e32 v100, v6
	v_sub_f32_e32 v6, v99, v133
	v_mul_f32_e32 v6, 0x3fb8aa3b, v6
	v_exp_f32_e32 v93, v6
	v_cvt_pk_bf16_f32 v162, v127, v96
	v_cvt_pk_bf16_f32 v163, v95, v100
	v_cvt_pk_bf16_f32 v164, v92, v91
	v_cvt_pk_bf16_f32 v165, v94, v93
	v_add_u32_e32 v7, 0x800, v8
	v_add_u32_e32 v6, 0x1000, v8
	s_waitcnt lgkmcnt(0)
	v_mfma_f32_16x16x32_bf16 v[182:185], v[158:161], v[162:165], 0
	v_lshl_add_u64 v[158:159], v[86:87], 0, v[70:71]
	ds_read2_b64 v[166:169], v7 offset0:32 offset1:36
	ds_read2_b64 v[178:181], v6 offset0:64 offset1:68
	v_lshl_add_u64 v[86:87], v[86:87], 0, v[80:81]
	v_lshl_add_u64 v[248:249], v[158:159], 0, 0
	v_lshl_add_u64 v[238:239], v[86:87], 0, 0
	global_load_dwordx4 v[186:189], v[158:159], off
	global_load_dwordx4 v[190:193], v[86:87], off
	global_load_dword v250, v[248:249], off offset:128
	global_load_dword v251, v[238:239], off offset:128
	v_sub_f32_e32 v9, v98, v133
	v_mul_f32_e32 v9, 0x3fb8aa3b, v9
	v_add_u32_e32 v158, 0x1800, v8
	v_exp_f32_e32 v86, v9
	v_sub_f32_e32 v9, v106, v133
	ds_read2_b64 v[194:197], v158 offset0:96 offset1:100
	v_mul_f32_e32 v9, 0x3fb8aa3b, v9
	v_exp_f32_e32 v76, v9
	v_sub_f32_e32 v9, v97, v133
	v_mul_f32_e32 v9, 0x3fb8aa3b, v9
	v_exp_f32_e32 v90, v9
	v_sub_f32_e32 v9, v104, v133
	v_mul_f32_e32 v9, 0x3fb8aa3b, v9
	v_exp_f32_e32 v87, v9
	v_sub_f32_e32 v9, v102, v133
	v_mul_f32_e32 v9, 0x3fb8aa3b, v9
	v_exp_f32_e32 v98, v9
	v_sub_f32_e32 v9, v110, v133
	v_mul_f32_e32 v9, 0x3fb8aa3b, v9
	v_add_u32_e32 v160, 0x4800, v8
	s_waitcnt lgkmcnt(2)
	v_mfma_f32_16x16x32_bf16 v[166:169], v[166:169], v[162:165], 0
	s_waitcnt vmcnt(7)
	ds_write_b128 v75, v[170:173] offset:18432
	s_waitcnt vmcnt(6)
	ds_write_b128 v75, v[174:177] offset:27648
	s_waitcnt lgkmcnt(0)
	s_barrier
; #define LAS __attribute__((address_space(3)))
; __device__ __forceinline__ unsigned cvt_pk_bf16(float lo, float hi) { const float __attribute__((ext_vector_type(2))) v = {lo, hi}; return __builtin_bit_cast(unsigned, __builtin_convertvector(v, bf16x2_t)); }
; template <bool LOCAL>
; __device__ __forceinline__ void na_unit(const bf16* P, const bf16* VT, bf16* YCAT, const LAS float* rpb_l, LAS bf16* buf, int b, int gr, int hp, int qblk, int tid) {
;     ...
;             const int c = sidx - NCH;
;             if (LOCAL && c < 8) {
;                 float p[8];
; #pragma unroll
;                 for (int e = 0; e < 4; ++e) { p[e] = __expf(sl[2 * (c < 8 ? c : 0)][e] - m); p[4 + e] = __expf(sl[2 * (c < 8 ? c : 0) + 1][e] - m); }
; #pragma unroll
;                 for (int e = 0; e < 8; ++e) lsum += p[e];
;                 const bf16x8 pf = __builtin_bit_cast(bf16x8, (v4u){pg8::cvt_pk_bf16(p[0], p[1]), pg8::cvt_pk_bf16(p[2], p[3]), pg8::cvt_pk_bf16(p[4], p[5]), pg8::cvt_pk_bf16(p[6], p[7])});
; #pragma unroll
;                 for (int dt = 0; dt < 4; ++dt) { const LAS bf16* vp = cb + (16 * dt + fr) * 72 + kc0 + 4 * fq;
;                     o[dt] = __builtin_amdgcn_mfma_f32_16x16x32_bf16(frag44(vp, vp + 16), pf, o[dt], 0, 0, 0); }
	v_mfma_f32_16x16x32_bf16 v[178:181], v[178:181], v[162:165], 0
	v_exp_f32_e32 v97, v9
	v_sub_f32_e32 v9, v101, v133
	v_mfma_f32_16x16x32_bf16 v[194:197], v[194:197], v[162:165], 0
	ds_read2_b64 v[162:165], v160 offset1:4
	v_mul_f32_e32 v9, 0x3fb8aa3b, v9
	v_add_u32_e32 v159, 0x5000, v8
	v_exp_f32_e32 v99, v9
	v_sub_f32_e32 v9, v108, v133
	ds_read2_b64 v[170:173], v159 offset0:32 offset1:36
	v_mul_f32_e32 v9, 0x3fb8aa3b, v9
	v_exp_f32_e32 v101, v9
	v_cvt_pk_bf16_f32 v174, v86, v90
	v_cvt_pk_bf16_f32 v175, v98, v99
	v_cvt_pk_bf16_f32 v176, v76, v87
	v_cvt_pk_bf16_f32 v177, v97, v101
	v_add_u32_e32 v161, 0x5800, v8
	v_sub_f32_e32 v9, v105, v133
	s_waitcnt lgkmcnt(1)
	v_mfma_f32_16x16x32_bf16 v[182:185], v[162:165], v[174:177], v[182:185]
	v_lshl_add_u64 v[162:163], s[0:1], 1, v[78:79]
	v_lshl_add_u64 v[198:199], v[162:163], 0, v[70:71]
	v_lshl_add_u64 v[162:163], v[162:163], 0, v[80:81]
	s_waitcnt lgkmcnt(0)
	v_mfma_f32_16x16x32_bf16 v[164:167], v[170:173], v[174:177], v[166:169]
	v_mul_f32_e32 v9, 0x3fb8aa3b, v9
	v_exp_f32_e32 v104, v9
	v_sub_f32_e32 v9, v114, v133
	ds_read2_b64 v[168:171], v161 offset0:64 offset1:68
	v_lshl_add_u64 v[248:249], v[198:199], 0, 0
	v_lshl_add_u64 v[238:239], v[162:163], 0, 0
	global_load_dwordx4 v[198:201], v[198:199], off
	s_nop 0
	global_load_dwordx4 v[202:205], v[162:163], off
	global_load_dword v250, v[248:249], off offset:128
	global_load_dword v251, v[238:239], off offset:128
	v_add_u32_e32 v162, 0x6000, v8
	s_waitcnt lgkmcnt(0)
	v_mfma_f32_16x16x32_bf16 v[168:171], v[168:171], v[174:177], v[178:181]
	s_nop 2
	ds_read2_b64 v[178:181], v162 offset0:96 offset1:100
	v_mul_f32_e32 v9, 0x3fb8aa3b, v9
	v_exp_f32_e32 v102, v9
	v_sub_f32_e32 v9, v103, v133
	v_mul_f32_e32 v9, 0x3fb8aa3b, v9
	v_exp_f32_e32 v105, v9
	v_sub_f32_e32 v9, v111, v133
	v_mul_f32_e32 v9, 0x3fb8aa3b, v9
	v_exp_f32_e32 v103, v9
	v_sub_f32_e32 v9, v109, v133
	v_mul_f32_e32 v9, 0x3fb8aa3b, v9
	v_exp_f32_e32 v108, v9
	v_sub_f32_e32 v9, v117, v133
	v_mul_f32_e32 v9, 0x3fb8aa3b, v9
	s_waitcnt lgkmcnt(0)
	v_mfma_f32_16x16x32_bf16 v[172:175], v[178:181], v[174:177], v[194:197]
	s_waitcnt vmcnt(7)
	ds_write_b128 v75, v[186:189]
	s_waitcnt vmcnt(6)
	ds_write_b128 v75, v[190:193] offset:9216
	s_waitcnt lgkmcnt(0)
	s_barrier
	v_exp_f32_e32 v106, v9
	v_sub_f32_e32 v9, v107, v133
	ds_read2_b64 v[176:179], v8 offset1:4
	ds_read2_b64 v[186:189], v7 offset0:32 offset1:36
	v_mul_f32_e32 v9, 0x3fb8aa3b, v9
	v_exp_f32_e32 v107, v9
	v_sub_f32_e32 v9, v113, v133
	v_mul_f32_e32 v9, 0x3fb8aa3b, v9
	v_exp_f32_e32 v109, v9
	v_lshl_add_u64 v[194:195], s[18:19], 1, v[78:79]
	v_cvt_pk_bf16_f32 v190, v104, v105
	v_cvt_pk_bf16_f32 v191, v108, v107
	v_cvt_pk_bf16_f32 v192, v102, v103
	v_cvt_pk_bf16_f32 v193, v106, v109
	v_lshl_add_u64 v[110:111], v[194:195], 0, v[70:71]
	v_lshl_add_u64 v[194:195], v[194:195], 0, v[80:81]
	s_waitcnt lgkmcnt(1)
	v_mfma_f32_16x16x32_bf16 v[176:179], v[176:179], v[190:193], v[182:185]
	v_sub_f32_e32 v9, v115, v133
	v_mul_f32_e32 v9, 0x3fb8aa3b, v9
	v_fma_f32 v62, v62, s66, -v133
	ds_read2_b64 v[180:183], v6 offset0:64 offset1:68
	s_waitcnt lgkmcnt(1)
	v_mfma_f32_16x16x32_bf16 v[164:167], v[186:189], v[190:193], v[164:167]
	v_lshl_add_u64 v[248:249], v[110:111], 0, 0
	v_lshl_add_u64 v[238:239], v[194:195], 0, 0
	global_load_dwordx4 v[184:187], v[110:111], off
	s_nop 0
	global_load_dwordx4 v[194:197], v[194:195], off
	global_load_dword v250, v[248:249], off offset:128
	global_load_dword v251, v[238:239], off offset:128
	v_exp_f32_e32 v111, v9
	v_sub_f32_e32 v9, v122, v133
	s_waitcnt lgkmcnt(0)
	v_mfma_f32_16x16x32_bf16 v[168:171], v[180:183], v[190:193], v[168:171]
	ds_read2_b64 v[180:183], v158 offset0:96 offset1:100
	v_mul_f32_e32 v9, 0x3fb8aa3b, v9
	v_exp_f32_e32 v110, v9
	v_sub_f32_e32 v9, v112, v133
	v_mul_f32_e32 v9, 0x3fb8aa3b, v9
	v_exp_f32_e32 v113, v9
	v_sub_f32_e32 v9, v119, v133
	v_mul_f32_e32 v9, 0x3fb8aa3b, v9
	v_exp_f32_e32 v112, v9
	v_sub_f32_e32 v9, v118, v133
	v_mul_f32_e32 v9, 0x3fb8aa3b, v9
	v_exp_f32_e32 v115, v9
	v_sub_f32_e32 v9, v125, v133
	v_mul_f32_e32 v9, 0x3fb8aa3b, v9
	s_waitcnt lgkmcnt(0)
	v_mfma_f32_16x16x32_bf16 v[172:175], v[180:183], v[190:193], v[172:175]
	s_waitcnt vmcnt(7)
	ds_write_b128 v75, v[198:201] offset:18432
	s_waitcnt vmcnt(6)
	ds_write_b128 v75, v[202:205] offset:27648
	s_waitcnt lgkmcnt(0)
	s_barrier
	v_exp_f32_e32 v114, v9
	v_sub_f32_e32 v9, v116, v133
	ds_read2_b64 v[180:183], v160 offset1:4
	ds_read2_b64 v[188:191], v159 offset0:32 offset1:36
	v_mul_f32_e32 v9, 0x3fb8aa3b, v9
	v_exp_f32_e32 v116, v9
	v_sub_f32_e32 v9, v121, v133
	v_mul_f32_e32 v9, 0x3fb8aa3b, v9
	v_exp_f32_e32 v117, v9
	v_lshl_add_u64 v[192:193], s[20:21], 1, v[78:79]
	v_lshl_add_u64 v[202:203], v[192:193], 0, v[70:71]
	v_cvt_pk_bf16_f32 v198, v111, v113
	v_cvt_pk_bf16_f32 v199, v115, v116
	v_cvt_pk_bf16_f32 v200, v110, v112
	v_cvt_pk_bf16_f32 v201, v114, v117
	v_lshl_add_u64 v[118:119], v[192:193], 0, v[80:81]
	v_sub_f32_e32 v9, v123, v133
	s_waitcnt lgkmcnt(1)
	v_mfma_f32_16x16x32_bf16 v[176:179], v[180:183], v[198:201], v[176:179]
	v_lshl_add_u64 v[248:249], v[202:203], 0, 0
	v_lshl_add_u64 v[238:239], v[118:119], 0, 0
	global_load_dwordx4 v[180:183], v[202:203], off
	s_nop 0
	global_load_dwordx4 v[202:205], v[118:119], off
	global_load_dword v250, v[248:249], off offset:128
	global_load_dword v251, v[238:239], off offset:128
	v_mul_f32_e32 v9, 0x3fb8aa3b, v9
	v_exp_f32_e32 v119, v9
	s_waitcnt lgkmcnt(0)
	v_mfma_f32_16x16x32_bf16 v[164:167], v[188:191], v[198:201], v[164:167]
	ds_read2_b64 v[188:191], v161 offset0:64 offset1:68
	v_sub_f32_e32 v9, v131, v133
	v_mul_f32_e32 v9, 0x3fb8aa3b, v9
	s_waitcnt lgkmcnt(0)
	v_mfma_f32_16x16x32_bf16 v[168:171], v[188:191], v[198:201], v[168:171]
	ds_read2_b64 v[188:191], v162 offset0:96 offset1:100
	v_exp_f32_e32 v118, v9
	v_sub_f32_e32 v9, v120, v133
	v_mul_f32_e32 v9, 0x3fb8aa3b, v9
	v_exp_f32_e32 v121, v9
	v_sub_f32_e32 v9, v128, v133
	v_mul_f32_e32 v9, 0x3fb8aa3b, v9
	v_exp_f32_e32 v120, v9
	v_sub_f32_e32 v9, v126, v133
	v_mul_f32_e32 v9, 0x3fb8aa3b, v9
	v_exp_f32_e32 v123, v9
	v_sub_f32_e32 v9, v135, v133
	v_mul_f32_e32 v9, 0x3fb8aa3b, v9
	s_waitcnt lgkmcnt(0)
	v_mfma_f32_16x16x32_bf16 v[172:175], v[188:191], v[198:201], v[172:175]
	s_waitcnt vmcnt(7)
	ds_write_b128 v75, v[184:187]
	s_waitcnt vmcnt(6)
	ds_write_b128 v75, v[194:197] offset:9216
	s_waitcnt lgkmcnt(0)
	s_barrier
; #define LAS __attribute__((address_space(3)))
; __device__ __forceinline__ unsigned cvt_pk_bf16(float lo, float hi) { const float __attribute__((ext_vector_type(2))) v = {lo, hi}; return __builtin_bit_cast(unsigned, __builtin_convertvector(v, bf16x2_t)); }
; template <bool LOCAL>
; __device__ __forceinline__ void na_unit(const bf16* P, const bf16* VT, bf16* YCAT, const LAS float* rpb_l, LAS bf16* buf, int b, int gr, int hp, int qblk, int tid) {
;     ...
;             if (LOCAL && c < 8) {
;                 float p[8];
; #pragma unroll
;                 for (int e = 0; e < 4; ++e) { p[e] = __expf(sl[2 * (c < 8 ? c : 0)][e] - m); p[4 + e] = __expf(sl[2 * (c < 8 ? c : 0) + 1][e] - m); }
; #pragma unroll
;                 for (int e = 0; e < 8; ++e) lsum += p[e];
;                 const bf16x8 pf = __builtin_bit_cast(bf16x8, (v4u){pg8::cvt_pk_bf16(p[0], p[1]), pg8::cvt_pk_bf16(p[2], p[3]), pg8::cvt_pk_bf16(p[4], p[5]), pg8::cvt_pk_bf16(p[6], p[7])});
; #pragma unroll
;                 for (int dt = 0; dt < 4; ++dt) { const LAS bf16* vp = cb + (16 * dt + fr) * 72 + kc0 + 4 * fq;
;                     o[dt] = __builtin_amdgcn_mfma_f32_16x16x32_bf16(frag44(vp, vp + 16), pf, o[dt], 0, 0, 0); }
;             } else {
;                 const int cc = c - NLOC;
; #pragma unroll
;                 for (int p2 = 0; p2 < 2; ++p2) {
;                     float p[8];
; #pragma unroll
;                     for (int e = 0; e < 4; ++e) { p[e] = __expf(sc[4 * (cc >= 0 ? cc : 0) + 2 * p2][e] - m); p[4 + e] = __expf(sc[4 * (cc >= 0 ? cc : 0) + 2 * p2 + 1][e] - m); }
; #pragma unroll
;                     for (int e = 0; e < 8; ++e) lsum += p[e];
;                     const bf16x8 pf = __builtin_bit_cast(bf16x8, (v4u){pg8::cvt_pk_bf16(p[0], p[1]), pg8::cvt_pk_bf16(p[2], p[3]), pg8::cvt_pk_bf16(p[4], p[5]), pg8::cvt_pk_bf16(p[6], p[7])});
; #pragma unroll
;                     for (int dt = 0; dt < 4; ++dt) { const LAS bf16* vp = cb + (16 * dt + fr) * 72 + 32 * p2 + 4 * fq;
;                         o[dt] = __builtin_amdgcn_mfma_f32_16x16x32_bf16(frag44(vp, vp + 16), pf, o[dt], 0, 0, 0); }
	v_exp_f32_e32 v122, v9
	v_sub_f32_e32 v9, v124, v133
	ds_read2_b64 v[184:187], v8 offset1:4
	ds_read2_b64 v[188:191], v7 offset0:32 offset1:36
	v_mul_f32_e32 v9, 0x3fb8aa3b, v9
	v_exp_f32_e32 v124, v9
	v_sub_f32_e32 v9, v130, v133
	v_mul_f32_e32 v9, 0x3fb8aa3b, v9
	v_exp_f32_e32 v125, v9
	v_lshl_add_u64 v[196:197], s[22:23], 1, v[78:79]
	v_cvt_pk_bf16_f32 v192, v119, v121
	v_cvt_pk_bf16_f32 v193, v123, v124
	v_cvt_pk_bf16_f32 v194, v118, v120
	v_cvt_pk_bf16_f32 v195, v122, v125
	v_lshl_add_u64 v[130:131], v[196:197], 0, v[70:71]
	v_lshl_add_u64 v[196:197], v[196:197], 0, v[80:81]
	s_waitcnt lgkmcnt(1)
	v_mfma_f32_16x16x32_bf16 v[176:179], v[184:187], v[192:195], v[176:179]
	ds_read2_b64 v[184:187], v6 offset0:64 offset1:68
	v_sub_f32_e32 v9, v132, v133
	v_mul_f32_e32 v9, 0x3fb8aa3b, v9
	s_waitcnt lgkmcnt(1)
	v_mfma_f32_16x16x32_bf16 v[164:167], v[188:191], v[192:195], v[164:167]
	v_lshl_add_u64 v[248:249], v[130:131], 0, 0
	v_lshl_add_u64 v[238:239], v[196:197], 0, 0
	global_load_dwordx4 v[188:191], v[130:131], off
	s_nop 0
	global_load_dwordx4 v[196:199], v[196:197], off
	global_load_dword v250, v[248:249], off offset:128
	global_load_dword v251, v[238:239], off offset:128
	v_exp_f32_e32 v128, v9
	v_sub_f32_e32 v9, v140, v133
	s_waitcnt lgkmcnt(0)
	v_mfma_f32_16x16x32_bf16 v[168:171], v[184:187], v[192:195], v[168:171]
	ds_read2_b64 v[184:187], v158 offset0:96 offset1:100
	v_mul_f32_e32 v9, 0x3fb8aa3b, v9
	v_exp_f32_e32 v126, v9
	v_sub_f32_e32 v9, v129, v133
	v_mul_f32_e32 v9, 0x3fb8aa3b, v9
	v_exp_f32_e32 v130, v9
	v_sub_f32_e32 v9, v137, v133
	v_mul_f32_e32 v9, 0x3fb8aa3b, v9
	v_exp_f32_e32 v129, v9
	v_sub_f32_e32 v9, v136, v133
	v_mul_f32_e32 v9, 0x3fb8aa3b, v9
	v_exp_f32_e32 v132, v9
	v_sub_f32_e32 v9, v143, v133
	v_mul_f32_e32 v9, 0x3fb8aa3b, v9
	s_waitcnt lgkmcnt(0)
	v_mfma_f32_16x16x32_bf16 v[172:175], v[184:187], v[192:195], v[172:175]
	s_waitcnt vmcnt(7)
	ds_write_b128 v75, v[180:183] offset:18432
	s_waitcnt vmcnt(6)
	ds_write_b128 v75, v[202:205] offset:27648
	s_waitcnt lgkmcnt(0)
	s_barrier
	v_exp_f32_e32 v131, v9
	v_sub_f32_e32 v9, v134, v133
	ds_read2_b64 v[180:183], v160 offset1:4
	ds_read2_b64 v[184:187], v159 offset0:32 offset1:36
	v_mul_f32_e32 v9, 0x3fb8aa3b, v9
	v_exp_f32_e32 v134, v9
	v_sub_f32_e32 v9, v139, v133
	v_mul_f32_e32 v9, 0x3fb8aa3b, v9
	v_exp_f32_e32 v135, v9
	v_lshl_add_u64 v[200:201], s[24:25], 1, v[78:79]
	v_lshl_add_u64 v[202:203], v[200:201], 0, v[70:71]
	v_cvt_pk_bf16_f32 v192, v128, v130
	v_cvt_pk_bf16_f32 v193, v132, v134
	v_cvt_pk_bf16_f32 v194, v126, v129
	v_cvt_pk_bf16_f32 v195, v131, v135
	v_lshl_add_u64 v[136:137], v[200:201], 0, v[80:81]
	v_sub_f32_e32 v9, v141, v133
	s_waitcnt lgkmcnt(1)
	v_mfma_f32_16x16x32_bf16 v[176:179], v[180:183], v[192:195], v[176:179]
	global_load_dwordx4 v[180:183], v[202:203], off
	s_nop 0
	global_load_dwordx4 v[200:203], v[136:137], off
	v_mul_f32_e32 v9, 0x3fb8aa3b, v9
	v_exp_f32_e32 v137, v9
	s_waitcnt lgkmcnt(0)
	v_mfma_f32_16x16x32_bf16 v[164:167], v[184:187], v[192:195], v[164:167]
	ds_read2_b64 v[184:187], v161 offset0:64 offset1:68
	v_sub_f32_e32 v9, v148, v133
	v_mul_f32_e32 v9, 0x3fb8aa3b, v9
	s_waitcnt lgkmcnt(0)
	v_mfma_f32_16x16x32_bf16 v[168:171], v[184:187], v[192:195], v[168:171]
	ds_read2_b64 v[184:187], v162 offset0:96 offset1:100
	v_exp_f32_e32 v136, v9
	v_sub_f32_e32 v9, v138, v133
	v_mul_f32_e32 v9, 0x3fb8aa3b, v9
	v_exp_f32_e32 v139, v9
	v_sub_f32_e32 v9, v145, v133
	v_mul_f32_e32 v9, 0x3fb8aa3b, v9
	v_exp_f32_e32 v138, v9
	v_sub_f32_e32 v9, v144, v133
	v_mul_f32_e32 v9, 0x3fb8aa3b, v9
	s_waitcnt lgkmcnt(0)
	v_mfma_f32_16x16x32_bf16 v[172:175], v[184:187], v[192:195], v[172:175]
	s_waitcnt vmcnt(5)
	ds_write_b128 v75, v[188:191]
	s_waitcnt vmcnt(4)
	ds_write_b128 v75, v[196:199] offset:9216
	s_waitcnt lgkmcnt(0)
	s_barrier
	v_exp_f32_e32 v141, v9
	v_sub_f32_e32 v9, v151, v133
	ds_read2_b64 v[184:187], v8 offset1:4
	v_mul_f32_e32 v9, 0x3fb8aa3b, v9
	ds_read2_b64 v[192:195], v7 offset0:32 offset1:36
	v_exp_f32_e32 v140, v9
	v_sub_f32_e32 v9, v142, v133
	v_sub_f32_e32 v8, v147, v133
	v_mul_f32_e32 v9, 0x3fb8aa3b, v9
	v_mul_f32_e32 v8, 0x3fb8aa3b, v8
	v_exp_f32_e32 v142, v9
	v_exp_f32_e32 v143, v8
	v_cvt_pk_bf16_f32 v188, v137, v139
	v_cvt_pk_bf16_f32 v190, v136, v138
	v_cvt_pk_bf16_f32 v189, v141, v142
	v_cvt_pk_bf16_f32 v191, v140, v143
	v_lshl_add_u64 v[8:9], s[26:27], 1, v[78:79]
	v_sub_f32_e32 v145, v150, v133
	s_waitcnt lgkmcnt(1)
	v_mfma_f32_16x16x32_bf16 v[176:179], v[184:187], v[188:191], v[176:179]
	ds_read2_b64 v[184:187], v6 offset0:64 offset1:68
	v_lshl_add_u64 v[6:7], v[8:9], 0, v[70:71]
	v_lshl_add_u64 v[8:9], v[8:9], 0, v[80:81]
	s_waitcnt lgkmcnt(1)
	v_mfma_f32_16x16x32_bf16 v[164:167], v[192:195], v[188:191], v[164:167]
	v_lshl_add_u64 v[248:249], v[6:7], 0, 0
	v_lshl_add_u64 v[238:239], v[8:9], 0, 0
	global_load_dwordx4 v[192:195], v[6:7], off
	global_load_dwordx4 v[196:199], v[8:9], off
	global_load_dword v250, v[248:249], off offset:128
	global_load_dword v251, v[238:239], off offset:128
	ds_read2_b64 v[78:81], v158 offset0:96 offset1:100
	s_waitcnt vmcnt(5)
	ds_write_b128 v75, v[180:183] offset:18432
	s_waitcnt vmcnt(4)
	ds_write_b128 v75, v[200:203] offset:27648
	s_waitcnt lgkmcnt(2)
	v_mfma_f32_16x16x32_bf16 v[172:175], v[78:81], v[188:191], v[172:175]
	s_waitcnt lgkmcnt(0)
	s_barrier
; #define LAS __attribute__((address_space(3)))
; __device__ __forceinline__ unsigned cvt_pk_bf16(float lo, float hi) { const float __attribute__((ext_vector_type(2))) v = {lo, hi}; return __builtin_bit_cast(unsigned, __builtin_convertvector(v, bf16x2_t)); }
; #define NA_STORE(sidx) do { LAS bf16* d_ = buf + ((sidx) & 1) * 9216; _Pragma("unroll") for (int q_ = 0; q_ < 2; ++q_) *(LAS v4u*)(d_ + q_ * 4608 + lrow * 72 + lseg * 8) = ld[(sidx) & 1][q_]; } while (0)
; template <bool LOCAL>
; __device__ __forceinline__ void na_unit(const bf16* P, const bf16* VT, bf16* YCAT, const LAS float* rpb_l, LAS bf16* buf, int b, int gr, int hp, int qblk, int tid) {
;     ...
;             } else {
;                 const int cc = c - NLOC;
; #pragma unroll
;                 for (int p2 = 0; p2 < 2; ++p2) {
;                     float p[8];
; #pragma unroll
;                     for (int e = 0; e < 4; ++e) { p[e] = __expf(sc[4 * (cc >= 0 ? cc : 0) + 2 * p2][e] - m); p[4 + e] = __expf(sc[4 * (cc >= 0 ? cc : 0) + 2 * p2 + 1][e] - m); }
; #pragma unroll
;                     for (int e = 0; e < 8; ++e) lsum += p[e];
;                     const bf16x8 pf = __builtin_bit_cast(bf16x8, (v4u){pg8::cvt_pk_bf16(p[0], p[1]), pg8::cvt_pk_bf16(p[2], p[3]), pg8::cvt_pk_bf16(p[4], p[5]), pg8::cvt_pk_bf16(p[6], p[7])});
; #pragma unroll
;                     for (int dt = 0; dt < 4; ++dt) { const LAS bf16* vp = cb + (16 * dt + fr) * 72 + 32 * p2 + 4 * fq;
;                         o[dt] = __builtin_amdgcn_mfma_f32_16x16x32_bf16(frag44(vp, vp + 16), pf, o[dt], 0, 0, 0); }
;                 }
;             }
;         }
;         if (sidx + 1 < 2 * NCH) NA_STORE(sidx + 1);
	v_sub_f32_e32 v70, v149, v133
	v_sub_f32_e32 v79, v146, v133
	v_sub_f32_e32 v81, v152, v133
	ds_read2_b64 v[148:151], v160 offset1:4
	v_mul_f32_e32 v70, 0x3fb8aa3b, v70
	v_mul_f32_e32 v79, 0x3fb8aa3b, v79
	v_mul_f32_e32 v81, 0x3fb8aa3b, v81
	v_mul_f32_e32 v145, 0x3fb8aa3b, v145
	v_exp_f32_e32 v78, v70
	v_sub_f32_e32 v70, v155, v133
	v_exp_f32_e32 v80, v79
	v_sub_f32_e32 v79, v153, v133
	v_exp_f32_e32 v144, v81
	v_sub_f32_e32 v81, v157, v133
	v_exp_f32_e32 v146, v145
	v_sub_f32_e32 v145, v154, v133
	v_mul_f32_e32 v70, 0x3fb8aa3b, v70
	v_mul_f32_e32 v79, 0x3fb8aa3b, v79
	v_mul_f32_e32 v81, 0x3fb8aa3b, v81
	v_mul_f32_e32 v145, 0x3fb8aa3b, v145
	v_exp_f32_e32 v70, v70
	v_exp_f32_e32 v79, v79
	v_exp_f32_e32 v81, v81
	v_exp_f32_e32 v145, v145
	v_cvt_pk_bf16_f32 v152, v78, v80
	v_cvt_pk_bf16_f32 v153, v144, v146
	v_cvt_pk_bf16_f32 v154, v70, v79
	v_cvt_pk_bf16_f32 v155, v81, v145
	v_mfma_f32_16x16x32_bf16 v[168:171], v[184:187], v[188:191], v[168:171]
	v_fma_f32 v63, v63, s66, -v133
	v_fma_f32 v64, v64, s66, -v133
	v_fma_f32 v65, v65, s66, -v133
	s_waitcnt lgkmcnt(0)
	v_mfma_f32_16x16x32_bf16 v[148:151], v[148:151], v[152:155], v[176:179]
	v_mul_f32_e32 v62, 0x3fb8aa3b, v62
	v_mul_f32_e32 v63, 0x3fb8aa3b, v63
	v_mul_f32_e32 v64, 0x3fb8aa3b, v64
	ds_read2_b64 v[176:179], v159 offset0:32 offset1:36
	ds_read2_b64 v[158:161], v161 offset0:64 offset1:68
	s_waitcnt lgkmcnt(0)
	v_mfma_f32_16x16x32_bf16 v[158:161], v[158:161], v[152:155], v[168:171]
	s_nop 2
	ds_read2_b64 v[168:171], v162 offset0:96 offset1:100
	v_mul_f32_e32 v65, 0x3fb8aa3b, v65
	v_exp_f32_e32 v147, v62
	v_mfma_f32_16x16x32_bf16 v[164:167], v[176:179], v[152:155], v[164:167]
	v_lshl_add_u64 v[248:249], v[6:7], 0, 0
	v_lshl_add_u64 v[238:239], v[8:9], 0, 0
	global_load_dwordx4 v[176:179], v[6:7], off offset:128
	global_load_dwordx4 v[180:183], v[8:9], off offset:128
	global_load_dword v250, v[248:249], off offset:256
	global_load_dword v251, v[238:239], off offset:256
	s_waitcnt vmcnt(7)
	ds_write_b128 v75, v[192:195]
	s_waitcnt vmcnt(6)
	ds_write_b128 v75, v[196:199] offset:9216
	s_waitcnt lgkmcnt(2)
	v_mfma_f32_16x16x32_bf16 v[152:155], v[168:171], v[152:155], v[172:175]
	s_waitcnt lgkmcnt(0)
	s_barrier
	ds_read2_b64 v[168:171], v156 offset1:4
	v_fma_f32 v62, v66, s66, -v133
	v_exp_f32_e32 v66, v63
	v_fma_f32 v63, v67, s66, -v133
	v_exp_f32_e32 v67, v64
	v_fma_f32 v64, v68, s66, -v133
	v_exp_f32_e32 v68, v65
	v_fma_f32 v65, v69, s66, -v133
	v_mul_f32_e32 v62, 0x3fb8aa3b, v62
	v_mul_f32_e32 v63, 0x3fb8aa3b, v63
	v_mul_f32_e32 v64, 0x3fb8aa3b, v64
	v_mul_f32_e32 v65, 0x3fb8aa3b, v65
	v_exp_f32_e32 v62, v62
	v_exp_f32_e32 v63, v63
	v_exp_f32_e32 v64, v64
	v_exp_f32_e32 v65, v65
	v_cvt_pk_bf16_f32 v172, v147, v66
	v_cvt_pk_bf16_f32 v173, v67, v68
	v_cvt_pk_bf16_f32 v174, v62, v63
	v_cvt_pk_bf16_f32 v175, v64, v65
	v_add_u32_e32 v157, 0x800, v156
	v_add_u32_e32 v192, 0x1000, v156
	s_waitcnt lgkmcnt(0)
	v_mfma_f32_16x16x32_bf16 v[148:151], v[168:171], v[172:175], v[148:151]
	ds_read2_b64 v[168:171], v157 offset0:32 offset1:36
	v_add_u32_e32 v193, 0x1800, v156
	v_fma_f32 v58, v58, s66, -v133
	s_waitcnt lgkmcnt(0)
	v_mfma_f32_16x16x32_bf16 v[162:165], v[168:171], v[172:175], v[164:167]
	s_nop 2
	ds_read2_b64 v[166:169], v192 offset0:64 offset1:68
	v_fma_f32 v54, v54, s66, -v133
	v_fma_f32 v59, v59, s66, -v133
	s_waitcnt lgkmcnt(0)
	v_mfma_f32_16x16x32_bf16 v[158:161], v[166:169], v[172:175], v[158:161]
	ds_read2_b64 v[166:169], v193 offset0:96 offset1:100
	v_fma_f32 v55, v55, s66, -v133
	v_fma_f32 v60, v60, s66, -v133
	s_waitcnt lgkmcnt(0)
	v_mfma_f32_16x16x32_bf16 v[152:155], v[166:169], v[172:175], v[152:155]
	ds_read2_b64 v[166:169], v156 offset0:8 offset1:12
	v_fma_f32 v56, v56, s66, -v133
	v_fma_f32 v61, v61, s66, -v133
	v_fma_f32 v57, v57, s66, -v133
	v_mul_f32_e32 v58, 0x3fb8aa3b, v58
	v_mul_f32_e32 v54, 0x3fb8aa3b, v54
	v_mul_f32_e32 v59, 0x3fb8aa3b, v59
	v_mul_f32_e32 v55, 0x3fb8aa3b, v55
	v_mul_f32_e32 v60, 0x3fb8aa3b, v60
	v_mul_f32_e32 v56, 0x3fb8aa3b, v56
	v_mul_f32_e32 v61, 0x3fb8aa3b, v61
	v_mul_f32_e32 v57, 0x3fb8aa3b, v57
	v_exp_f32_e32 v58, v58
	v_exp_f32_e32 v54, v54
	v_exp_f32_e32 v59, v59
	v_exp_f32_e32 v55, v55
	v_exp_f32_e32 v60, v60
	v_exp_f32_e32 v56, v56
	v_exp_f32_e32 v61, v61
	v_exp_f32_e32 v57, v57
	v_cvt_pk_bf16_f32 v170, v58, v59
	v_cvt_pk_bf16_f32 v172, v54, v55
	v_cvt_pk_bf16_f32 v171, v60, v61
	v_cvt_pk_bf16_f32 v173, v56, v57
	v_fma_f32 v46, v46, s66, -v133
	v_fma_f32 v47, v47, s66, -v133
	s_waitcnt lgkmcnt(0)
	v_mfma_f32_16x16x32_bf16 v[148:151], v[166:169], v[170:173], v[148:151]
	ds_read2_b64 v[166:169], v157 offset0:40 offset1:44
	v_fma_f32 v48, v48, s66, -v133
	v_mul_f32_e32 v46, 0x3fb8aa3b, v46
	s_waitcnt lgkmcnt(0)
	v_mfma_f32_16x16x32_bf16 v[162:165], v[166:169], v[170:173], v[162:165]
	ds_read2_b64 v[166:169], v192 offset0:72 offset1:76
	v_mul_f32_e32 v47, 0x3fb8aa3b, v47
	v_mul_f32_e32 v48, 0x3fb8aa3b, v48
	s_waitcnt lgkmcnt(0)
	v_mfma_f32_16x16x32_bf16 v[158:161], v[166:169], v[170:173], v[158:161]
	ds_read2_b64 v[166:169], v193 offset0:104 offset1:108
	v_exp_f32_e32 v69, v46
	v_fma_f32 v46, v50, s66, -v133
	v_exp_f32_e32 v50, v47
	v_fma_f32 v47, v51, s66, -v133
	v_exp_f32_e32 v51, v48
	v_fma_f32 v48, v52, s66, -v133
	v_add_u32_e32 v52, 0x4800, v156
	v_lshl_add_u64 v[248:249], v[6:7], 0, 0
	v_lshl_add_u64 v[238:239], v[8:9], 0, 0
	global_load_dwordx4 v[184:187], v[6:7], off offset:256
	global_load_dwordx4 v[188:191], v[8:9], off offset:256
	global_load_dword v250, v[248:249], off offset:384
	global_load_dword v251, v[238:239], off offset:384
	s_waitcnt lgkmcnt(0)
	v_mfma_f32_16x16x32_bf16 v[152:155], v[166:169], v[170:173], v[152:155]
	s_waitcnt vmcnt(7)
	ds_write_b128 v75, v[176:179] offset:18432
	s_waitcnt vmcnt(6)
	ds_write_b128 v75, v[180:183] offset:27648
	s_waitcnt lgkmcnt(0)
	s_barrier
; #define LAS __attribute__((address_space(3)))
; __device__ __forceinline__ unsigned cvt_pk_bf16(float lo, float hi) { const float __attribute__((ext_vector_type(2))) v = {lo, hi}; return __builtin_bit_cast(unsigned, __builtin_convertvector(v, bf16x2_t)); }
; #define NA_STORE(sidx) do { LAS bf16* d_ = buf + ((sidx) & 1) * 9216; _Pragma("unroll") for (int q_ = 0; q_ < 2; ++q_) *(LAS v4u*)(d_ + q_ * 4608 + lrow * 72 + lseg * 8) = ld[(sidx) & 1][q_]; } while (0)
; template <bool LOCAL>
; __device__ __forceinline__ void na_unit(const bf16* P, const bf16* VT, bf16* YCAT, const LAS float* rpb_l, LAS bf16* buf, int b, int gr, int hp, int qblk, int tid) {
;     ...
;             } else {
;                 const int cc = c - NLOC;
; #pragma unroll
;                 for (int p2 = 0; p2 < 2; ++p2) {
;                     float p[8];
; #pragma unroll
;                     for (int e = 0; e < 4; ++e) { p[e] = __expf(sc[4 * (cc >= 0 ? cc : 0) + 2 * p2][e] - m); p[4 + e] = __expf(sc[4 * (cc >= 0 ? cc : 0) + 2 * p2 + 1][e] - m); }
; #pragma unroll
;                     for (int e = 0; e < 8; ++e) lsum += p[e];
;                     const bf16x8 pf = __builtin_bit_cast(bf16x8, (v4u){pg8::cvt_pk_bf16(p[0], p[1]), pg8::cvt_pk_bf16(p[2], p[3]), pg8::cvt_pk_bf16(p[4], p[5]), pg8::cvt_pk_bf16(p[6], p[7])});
; #pragma unroll
;                     for (int dt = 0; dt < 4; ++dt) { const LAS bf16* vp = cb + (16 * dt + fr) * 72 + 32 * p2 + 4 * fq;
;                         o[dt] = __builtin_amdgcn_mfma_f32_16x16x32_bf16(frag44(vp, vp + 16), pf, o[dt], 0, 0, 0); }
;                 }
;             }
;         }
;         if (sidx + 1 < 2 * NCH) NA_STORE(sidx + 1);
;         __syncthreads();
	v_fma_f32 v49, v49, s66, -v133
	ds_read2_b64 v[166:169], v52 offset1:4
	v_mul_f32_e32 v49, 0x3fb8aa3b, v49
	v_exp_f32_e32 v174, v49
	v_fma_f32 v49, v53, s66, -v133
	v_mul_f32_e32 v46, 0x3fb8aa3b, v46
	v_mul_f32_e32 v47, 0x3fb8aa3b, v47
	v_mul_f32_e32 v48, 0x3fb8aa3b, v48
	v_mul_f32_e32 v49, 0x3fb8aa3b, v49
	v_exp_f32_e32 v46, v46
	v_exp_f32_e32 v47, v47
	v_exp_f32_e32 v48, v48
	v_exp_f32_e32 v53, v49
	v_cvt_pk_bf16_f32 v170, v69, v50
	v_cvt_pk_bf16_f32 v171, v51, v174
	v_cvt_pk_bf16_f32 v172, v46, v47
	v_cvt_pk_bf16_f32 v173, v48, v53
	v_add_u32_e32 v175, 0x5000, v156
	v_add_u32_e32 v176, 0x5800, v156
	s_waitcnt lgkmcnt(0)
	v_mfma_f32_16x16x32_bf16 v[148:151], v[166:169], v[170:173], v[148:151]
	ds_read2_b64 v[166:169], v175 offset0:32 offset1:36
	v_add_u32_e32 v49, 0x6000, v156
	v_fma_f32 v38, v38, s66, -v133
	s_waitcnt lgkmcnt(0)
	v_mfma_f32_16x16x32_bf16 v[162:165], v[166:169], v[170:173], v[162:165]
	ds_read2_b64 v[166:169], v176 offset0:64 offset1:68
	v_mul_f32_e32 v38, 0x3fb8aa3b, v38
	v_fma_f32 v42, v42, s66, -v133
	s_waitcnt lgkmcnt(0)
	v_mfma_f32_16x16x32_bf16 v[158:161], v[166:169], v[170:173], v[158:161]
	ds_read2_b64 v[166:169], v49 offset0:96 offset1:100
	v_mul_f32_e32 v42, 0x3fb8aa3b, v42
	v_fma_f32 v30, v30, s66, -v133
	s_waitcnt lgkmcnt(0)
	v_mfma_f32_16x16x32_bf16 v[152:155], v[166:169], v[170:173], v[152:155]
	v_exp_f32_e32 v171, v38
	v_fma_f32 v38, v43, s66, -v133
	v_mul_f32_e32 v38, 0x3fb8aa3b, v38
	v_exp_f32_e32 v172, v38
	v_fma_f32 v38, v39, s66, -v133
	v_mul_f32_e32 v38, 0x3fb8aa3b, v38
	v_exp_f32_e32 v173, v38
	v_fma_f32 v38, v44, s66, -v133
	v_mul_f32_e32 v38, 0x3fb8aa3b, v38
	v_exp_f32_e32 v177, v38
	v_fma_f32 v38, v40, s66, -v133
	v_mul_f32_e32 v38, 0x3fb8aa3b, v38
	v_exp_f32_e32 v170, v42
	v_exp_f32_e32 v178, v38
	v_fma_f32 v38, v45, s66, -v133
	ds_read2_b64 v[42:45], v52 offset0:8 offset1:12
	v_mul_f32_e32 v38, 0x3fb8aa3b, v38
	v_exp_f32_e32 v179, v38
	v_fma_f32 v38, v41, s66, -v133
	v_mul_f32_e32 v38, 0x3fb8aa3b, v38
	v_exp_f32_e32 v180, v38
	v_cvt_pk_bf16_f32 v38, v170, v172
	v_cvt_pk_bf16_f32 v39, v177, v179
	v_cvt_pk_bf16_f32 v40, v171, v173
	v_cvt_pk_bf16_f32 v41, v178, v180
	v_mul_f32_e32 v30, 0x3fb8aa3b, v30
	v_fma_f32 v22, v22, s66, -v133
	s_waitcnt lgkmcnt(0)
	v_mfma_f32_16x16x32_bf16 v[42:45], v[42:45], v[38:41], v[148:151]
	v_mul_f32_e32 v22, 0x3fb8aa3b, v22
	v_fma_f32 v26, v26, s66, -v133
	v_mul_f32_e32 v26, 0x3fb8aa3b, v26
	ds_read2_b64 v[148:151], v175 offset0:40 offset1:44
	s_waitcnt lgkmcnt(0)
	v_mfma_f32_16x16x32_bf16 v[148:151], v[148:151], v[38:41], v[162:165]
	s_nop 2
	ds_read2_b64 v[162:165], v176 offset0:72 offset1:76
	v_fma_f32 v2, v2, s66, -v133
	v_mul_f32_e32 v2, 0x3fb8aa3b, v2
	s_waitcnt lgkmcnt(0)
	v_mfma_f32_16x16x32_bf16 v[158:161], v[162:165], v[38:41], v[158:161]
	ds_read2_b64 v[162:165], v49 offset0:104 offset1:108
	global_load_dwordx4 v[166:169], v[6:7], off offset:384
	s_nop 0
	global_load_dwordx4 v[6:9], v[8:9], off offset:384
	s_waitcnt vmcnt(5)
	ds_write_b128 v75, v[184:187]
	s_waitcnt vmcnt(4)
	ds_write_b128 v75, v[188:191] offset:9216
	s_waitcnt lgkmcnt(2)
	v_mfma_f32_16x16x32_bf16 v[38:41], v[162:165], v[38:41], v[152:155]
	v_exp_f32_e32 v162, v30
	v_fma_f32 v30, v34, s66, -v133
	v_mul_f32_e32 v30, 0x3fb8aa3b, v30
	v_exp_f32_e32 v163, v30
	v_fma_f32 v30, v31, s66, -v133
	v_mul_f32_e32 v30, 0x3fb8aa3b, v30
	v_exp_f32_e32 v164, v30
	v_fma_f32 v30, v35, s66, -v133
	v_mul_f32_e32 v30, 0x3fb8aa3b, v30
	v_exp_f32_e32 v165, v30
	v_fma_f32 v30, v32, s66, -v133
	v_mul_f32_e32 v30, 0x3fb8aa3b, v30
	v_exp_f32_e32 v181, v30
	v_fma_f32 v30, v36, s66, -v133
	v_mul_f32_e32 v30, 0x3fb8aa3b, v30
	v_exp_f32_e32 v182, v30
	v_fma_f32 v30, v33, s66, -v133
	s_waitcnt lgkmcnt(0)
	s_barrier
	v_mul_f32_e32 v34, 0x3fb8aa3b, v30
	ds_read2_b64 v[30:33], v156 offset1:4
	v_exp_f32_e32 v183, v34
	v_fma_f32 v34, v37, s66, -v133
	v_mul_f32_e32 v34, 0x3fb8aa3b, v34
	v_exp_f32_e32 v184, v34
	v_cvt_pk_bf16_f32 v34, v162, v164
	v_cvt_pk_bf16_f32 v35, v181, v183
	v_cvt_pk_bf16_f32 v36, v163, v165
	v_cvt_pk_bf16_f32 v37, v182, v184
	ds_read2_b64 v[152:155], v193 offset0:96 offset1:100
	v_fma_f32 v10, v10, s66, -v133
	s_waitcnt lgkmcnt(1)
	v_mfma_f32_16x16x32_bf16 v[30:33], v[30:33], v[34:37], v[42:45]
	v_mul_f32_e32 v10, 0x3fb8aa3b, v10
	s_nop 1
	ds_read2_b64 v[42:45], v157 offset0:32 offset1:36
	s_waitcnt lgkmcnt(0)
	v_mfma_f32_16x16x32_bf16 v[42:45], v[42:45], v[34:37], v[148:151]
	s_nop 2
	ds_read2_b64 v[148:151], v192 offset0:64 offset1:68
	s_waitcnt lgkmcnt(0)
	v_mfma_f32_16x16x32_bf16 v[148:151], v[148:151], v[34:37], v[158:161]
	v_mfma_f32_16x16x32_bf16 v[34:37], v[152:155], v[34:37], v[38:41]
	v_exp_f32_e32 v153, v22
	v_fma_f32 v22, v27, s66, -v133
	v_mul_f32_e32 v22, 0x3fb8aa3b, v22
	v_exp_f32_e32 v154, v22
	v_fma_f32 v22, v23, s66, -v133
	v_mul_f32_e32 v22, 0x3fb8aa3b, v22
	v_exp_f32_e32 v155, v22
	v_fma_f32 v22, v28, s66, -v133
	v_mul_f32_e32 v22, 0x3fb8aa3b, v22
	v_exp_f32_e32 v158, v22
	v_fma_f32 v22, v24, s66, -v133
	v_mul_f32_e32 v22, 0x3fb8aa3b, v22
	v_exp_f32_e32 v152, v26
	v_exp_f32_e32 v159, v22
	v_fma_f32 v22, v29, s66, -v133
	ds_read2_b64 v[26:29], v156 offset0:8 offset1:12
	v_mul_f32_e32 v22, 0x3fb8aa3b, v22
	v_exp_f32_e32 v156, v22
	v_fma_f32 v22, v25, s66, -v133
	v_mul_f32_e32 v22, 0x3fb8aa3b, v22
	v_exp_f32_e32 v160, v22
	v_cvt_pk_bf16_f32 v22, v152, v154
	v_cvt_pk_bf16_f32 v23, v158, v156
	v_cvt_pk_bf16_f32 v24, v153, v155
	v_cvt_pk_bf16_f32 v25, v159, v160
	ds_read2_b64 v[38:41], v192 offset0:72 offset1:76
	s_waitcnt lgkmcnt(1)
	v_mfma_f32_16x16x32_bf16 v[26:29], v[26:29], v[22:25], v[30:33]
	s_nop 2
	ds_read2_b64 v[30:33], v157 offset0:40 offset1:44
	s_waitcnt lgkmcnt(0)
	v_mfma_f32_16x16x32_bf16 v[30:33], v[30:33], v[22:25], v[42:45]
	s_nop 2
	ds_read2_b64 v[42:45], v193 offset0:104 offset1:108
	s_waitcnt vmcnt(1)
	ds_write_b128 v75, v[166:169] offset:18432
	s_waitcnt vmcnt(0)
	ds_write_b128 v75, v[6:9] offset:27648
	v_fma_f32 v6, v14, s66, -v133
	v_mul_f32_e32 v6, 0x3fb8aa3b, v6
	v_mfma_f32_16x16x32_bf16 v[38:41], v[38:41], v[22:25], v[148:151]
	s_waitcnt lgkmcnt(0)
	s_barrier
; #define LAS __attribute__((address_space(3)))
; __device__ __forceinline__ unsigned cvt_pk_bf16(float lo, float hi) { const float __attribute__((ext_vector_type(2))) v = {lo, hi}; return __builtin_bit_cast(unsigned, __builtin_convertvector(v, bf16x2_t)); }
; #define NA_STORE(sidx) do { LAS bf16* d_ = buf + ((sidx) & 1) * 9216; _Pragma("unroll") for (int q_ = 0; q_ < 2; ++q_) *(LAS v4u*)(d_ + q_ * 4608 + lrow * 72 + lseg * 8) = ld[(sidx) & 1][q_]; } while (0)
; template <bool LOCAL>
; __device__ __forceinline__ void na_unit(const bf16* P, const bf16* VT, bf16* YCAT, const LAS float* rpb_l, LAS bf16* buf, int b, int gr, int hp, int qblk, int tid) {
;     ...
;                 const int cc = c - NLOC;
; #pragma unroll
;                 for (int p2 = 0; p2 < 2; ++p2) {
;                     float p[8];
; #pragma unroll
;                     for (int e = 0; e < 4; ++e) { p[e] = __expf(sc[4 * (cc >= 0 ? cc : 0) + 2 * p2][e] - m); p[4 + e] = __expf(sc[4 * (cc >= 0 ? cc : 0) + 2 * p2 + 1][e] - m); }
; #pragma unroll
;                     for (int e = 0; e < 8; ++e) lsum += p[e];
;                     const bf16x8 pf = __builtin_bit_cast(bf16x8, (v4u){pg8::cvt_pk_bf16(p[0], p[1]), pg8::cvt_pk_bf16(p[2], p[3]), pg8::cvt_pk_bf16(p[4], p[5]), pg8::cvt_pk_bf16(p[6], p[7])});
; #pragma unroll
;                     for (int dt = 0; dt < 4; ++dt) { const LAS bf16* vp = cb + (16 * dt + fr) * 72 + 32 * p2 + 4 * fq;
;                         o[dt] = __builtin_amdgcn_mfma_f32_16x16x32_bf16(frag44(vp, vp + 16), pf, o[dt], 0, 0, 0); }
;                 }
;             }
;         }
;         if (sidx + 1 < 2 * NCH) NA_STORE(sidx + 1);
;         __syncthreads();
;     }
;     ...
;     lsum += __shfl_xor(lsum, 16); lsum += __shfl_xor(lsum, 32);
	v_mfma_f32_16x16x32_bf16 v[22:25], v[42:45], v[22:25], v[34:37]
	v_ashrrev_i32_e32 v75, 31, v74
	s_nop 1
	v_exp_f32_e32 v34, v6
	v_fma_f32 v6, v18, s66, -v133
	v_mul_f32_e32 v6, 0x3fb8aa3b, v6
	v_exp_f32_e32 v35, v6
	v_fma_f32 v6, v15, s66, -v133
	v_mul_f32_e32 v6, 0x3fb8aa3b, v6
	v_exp_f32_e32 v36, v6
	v_fma_f32 v6, v19, s66, -v133
	v_mul_f32_e32 v6, 0x3fb8aa3b, v6
	v_exp_f32_e32 v37, v6
	v_fma_f32 v6, v16, s66, -v133
	v_mul_f32_e32 v6, 0x3fb8aa3b, v6
	v_exp_f32_e32 v42, v6
	v_fma_f32 v6, v20, s66, -v133
	v_mul_f32_e32 v6, 0x3fb8aa3b, v6
	v_exp_f32_e32 v43, v6
	v_fma_f32 v6, v17, s66, -v133
	v_mul_f32_e32 v14, 0x3fb8aa3b, v6
	ds_read2_b64 v[6:9], v52 offset1:4
	v_exp_f32_e32 v44, v14
	v_fma_f32 v14, v21, s66, -v133
	v_mul_f32_e32 v14, 0x3fb8aa3b, v14
	v_exp_f32_e32 v45, v14
	v_cvt_pk_bf16_f32 v14, v34, v36
	v_cvt_pk_bf16_f32 v15, v42, v44
	v_cvt_pk_bf16_f32 v16, v35, v37
	v_cvt_pk_bf16_f32 v17, v43, v45
	ds_read2_b64 v[18:21], v175 offset0:32 offset1:36
	s_waitcnt lgkmcnt(1)
	v_mfma_f32_16x16x32_bf16 v[6:9], v[6:9], v[14:17], v[26:29]
	s_nop 2
	ds_read2_b64 v[26:29], v176 offset0:64 offset1:68
	s_waitcnt lgkmcnt(0)
	v_mfma_f32_16x16x32_bf16 v[26:29], v[26:29], v[14:17], v[38:41]
	s_nop 2
	v_add_f32_e32 v38, 0, v127
	v_add_f32_e32 v38, v96, v38
	v_add_f32_e32 v38, v95, v38
	v_add_f32_e32 v38, v100, v38
	v_add_f32_e32 v38, v92, v38
	v_add_f32_e32 v38, v91, v38
	v_add_f32_e32 v38, v94, v38
	v_add_f32_e32 v38, v93, v38
	v_add_f32_e32 v38, v86, v38
	v_add_f32_e32 v38, v90, v38
	v_add_f32_e32 v38, v98, v38
	v_add_f32_e32 v38, v99, v38
	v_add_f32_e32 v38, v76, v38
	v_add_f32_e32 v38, v87, v38
	v_add_f32_e32 v38, v97, v38
	v_add_f32_e32 v38, v101, v38
	v_add_f32_e32 v38, v104, v38
	v_add_f32_e32 v38, v105, v38
	v_add_f32_e32 v38, v108, v38
	v_add_f32_e32 v38, v107, v38
	v_add_f32_e32 v38, v102, v38
	v_add_f32_e32 v38, v103, v38
	v_add_f32_e32 v38, v106, v38
	v_add_f32_e32 v38, v109, v38
	v_add_f32_e32 v38, v111, v38
	v_add_f32_e32 v38, v113, v38
	v_add_f32_e32 v38, v115, v38
	v_add_f32_e32 v38, v116, v38
	v_add_f32_e32 v38, v110, v38
	v_add_f32_e32 v38, v112, v38
	v_add_f32_e32 v38, v114, v38
	v_add_f32_e32 v38, v117, v38
	v_add_f32_e32 v38, v119, v38
	v_add_f32_e32 v38, v121, v38
	v_add_f32_e32 v38, v123, v38
	v_add_f32_e32 v38, v124, v38
	v_add_f32_e32 v38, v118, v38
	v_add_f32_e32 v38, v120, v38
	v_add_f32_e32 v38, v122, v38
	v_add_f32_e32 v38, v125, v38
	v_add_f32_e32 v38, v128, v38
	v_add_f32_e32 v38, v130, v38
	v_add_f32_e32 v38, v132, v38
	v_add_f32_e32 v38, v134, v38
	v_add_f32_e32 v38, v126, v38
	v_add_f32_e32 v38, v129, v38
	v_add_f32_e32 v38, v131, v38
	v_add_f32_e32 v38, v135, v38
	v_add_f32_e32 v38, v137, v38
	v_add_f32_e32 v38, v139, v38
	v_add_f32_e32 v38, v141, v38
	v_add_f32_e32 v38, v142, v38
	v_add_f32_e32 v38, v136, v38
	v_add_f32_e32 v38, v138, v38
	v_add_f32_e32 v38, v140, v38
	v_add_f32_e32 v38, v143, v38
	v_add_f32_e32 v38, v78, v38
	v_add_f32_e32 v38, v80, v38
	v_add_f32_e32 v38, v144, v38
	v_add_f32_e32 v38, v146, v38
	v_add_f32_e32 v38, v70, v38
	v_add_f32_e32 v38, v79, v38
	v_add_f32_e32 v38, v81, v38
	v_add_f32_e32 v38, v145, v38
	v_add_f32_e32 v38, v147, v38
	v_add_f32_e32 v38, v66, v38
	v_add_f32_e32 v38, v67, v38
	v_add_f32_e32 v38, v68, v38
	v_add_f32_e32 v38, v62, v38
	v_add_f32_e32 v38, v63, v38
	v_add_f32_e32 v38, v64, v38
	v_add_f32_e32 v38, v65, v38
	v_add_f32_e32 v38, v58, v38
	v_add_f32_e32 v38, v59, v38
	v_add_f32_e32 v38, v60, v38
	v_add_f32_e32 v38, v61, v38
	v_add_f32_e32 v38, v54, v38
	v_add_f32_e32 v38, v55, v38
	v_add_f32_e32 v38, v56, v38
	v_add_f32_e32 v38, v57, v38
	v_add_f32_e32 v38, v69, v38
	v_add_f32_e32 v38, v50, v38
	v_add_f32_e32 v38, v51, v38
	v_add_f32_e32 v38, v174, v38
	v_add_f32_e32 v38, v46, v38
	v_add_f32_e32 v38, v47, v38
	v_add_f32_e32 v38, v48, v38
	v_add_f32_e32 v38, v53, v38
	v_add_f32_e32 v38, v170, v38
	v_mfma_f32_16x16x32_bf16 v[18:21], v[18:21], v[14:17], v[30:33]
	v_add_f32_e32 v38, v172, v38
	v_add_f32_e32 v38, v177, v38
	v_add_f32_e32 v38, v179, v38
	ds_read2_b64 v[30:33], v49 offset0:96 offset1:100
	v_add_f32_e32 v38, v171, v38
	v_add_f32_e32 v38, v173, v38
	v_add_f32_e32 v38, v178, v38
	v_add_f32_e32 v38, v180, v38
	v_add_f32_e32 v38, v162, v38
	v_add_f32_e32 v38, v164, v38
	s_waitcnt lgkmcnt(0)
	v_mfma_f32_16x16x32_bf16 v[14:17], v[30:33], v[14:17], v[22:25]
	v_add_f32_e32 v38, v181, v38
	s_nop 1
	v_exp_f32_e32 v23, v2
	v_fma_f32 v2, v11, s66, -v133
	v_mul_f32_e32 v2, 0x3fb8aa3b, v2
	v_add_f32_e32 v38, v183, v38
	v_exp_f32_e32 v24, v2
	v_fma_f32 v2, v3, s66, -v133
	v_add_f32_e32 v38, v163, v38
	v_mul_f32_e32 v2, 0x3fb8aa3b, v2
	v_add_f32_e32 v38, v165, v38
	v_exp_f32_e32 v25, v2
	v_fma_f32 v2, v12, s66, -v133
	v_add_f32_e32 v38, v182, v38
	v_mul_f32_e32 v2, 0x3fb8aa3b, v2
	v_add_f32_e32 v38, v184, v38
	v_exp_f32_e32 v30, v2
	v_fma_f32 v2, v4, s66, -v133
	v_add_f32_e32 v38, v152, v38
	v_mul_f32_e32 v2, 0x3fb8aa3b, v2
	v_add_f32_e32 v38, v154, v38
	v_exp_f32_e32 v22, v10
	v_exp_f32_e32 v31, v2
	v_fma_f32 v2, v13, s66, -v133
	ds_read2_b64 v[10:13], v52 offset0:8 offset1:12
	v_add_f32_e32 v38, v158, v38
	v_mul_f32_e32 v2, 0x3fb8aa3b, v2
	v_add_f32_e32 v38, v156, v38
	v_exp_f32_e32 v32, v2
	v_fma_f32 v2, v5, s66, -v133
	v_add_f32_e32 v38, v153, v38
	v_mul_f32_e32 v2, 0x3fb8aa3b, v2
	v_add_f32_e32 v38, v155, v38
	v_exp_f32_e32 v33, v2
	v_add_f32_e32 v38, v159, v38
	v_add_f32_e32 v38, v160, v38
	v_add_f32_e32 v34, v34, v38
	v_add_f32_e32 v34, v36, v34
	v_cvt_pk_bf16_f32 v2, v22, v24
	v_cvt_pk_bf16_f32 v3, v30, v32
	v_cvt_pk_bf16_f32 v4, v23, v25
	v_cvt_pk_bf16_f32 v5, v31, v33
	v_add_f32_e32 v34, v42, v34
	v_add_f32_e32 v34, v44, v34
	s_waitcnt lgkmcnt(0)
	v_mfma_f32_16x16x32_bf16 v[6:9], v[10:13], v[2:5], v[6:9]
	ds_read2_b64 v[10:13], v175 offset0:40 offset1:44
	v_add_f32_e32 v34, v35, v34
	v_add_f32_e32 v34, v37, v34
	v_add_f32_e32 v34, v43, v34
	v_add_f32_e32 v34, v45, v34
	v_add_f32_e32 v22, v22, v34
	v_add_f32_e32 v22, v24, v22
	v_add_f32_e32 v22, v30, v22
	v_add_f32_e32 v22, v32, v22
	s_waitcnt lgkmcnt(0)
	v_mfma_f32_16x16x32_bf16 v[10:13], v[10:13], v[2:5], v[18:21]
	v_add_f32_e32 v22, v23, v22
	v_add_f32_e32 v22, v25, v22
	v_add_f32_e32 v22, v31, v22
	ds_read2_b64 v[18:21], v176 offset0:72 offset1:76
	v_add_f32_e32 v30, v33, v22
	ds_bpermute_b32 v31, v88, v30
	ds_read2_b64 v[22:25], v49 offset0:104 offset1:108
	s_waitcnt lgkmcnt(2)
	v_mfma_f32_16x16x32_bf16 v[18:21], v[18:21], v[2:5], v[26:29]
	s_waitcnt lgkmcnt(1)
	s_nop 1
	v_add_f32_e32 v26, v30, v31
	ds_bpermute_b32 v27, v89, v26
	v_lshlrev_b32_e32 v70, 1, v77
	s_waitcnt lgkmcnt(1)
	v_mfma_f32_16x16x32_bf16 v[14:17], v[22:25], v[2:5], v[14:17]
	s_waitcnt lgkmcnt(0)
	s_barrier
; __device__ __forceinline__ unsigned cvt_pk_bf16(float lo, float hi) { const float __attribute__((ext_vector_type(2))) v = {lo, hi}; return __builtin_bit_cast(unsigned, __builtin_convertvector(v, bf16x2_t)); }
; template <bool LOCAL>
; __device__ __forceinline__ void na_unit(const bf16* P, const bf16* VT, bf16* YCAT, const LAS float* rpb_l, LAS bf16* buf, int b, int gr, int hp, int qblk, int tid) {
;     ...
;     lsum += __shfl_xor(lsum, 16); lsum += __shfl_xor(lsum, 32);
;     const float inv = 1.f / lsum;
;     bf16* op = YCAT + (size_t)(qrow0 + fr) * D + 512 + h * 64 + 4 * fq;
; #pragma unroll
;     for (int dt = 0; dt < 4; ++dt) { v2u w; w.x = pg8::cvt_pk_bf16(o[dt][0] * inv, o[dt][1] * inv); w.y = pg8::cvt_pk_bf16(o[dt][2] * inv, o[dt][3] * inv); *(v2u*)(op + dt * 16) = w; }
	v_add_f32_e32 v2, v26, v27
	v_div_scale_f32 v3, s[0:1], v2, v2, 1.0
	v_rcp_f32_e32 v4, v3
	s_nop 0
	v_fma_f32 v5, -v3, v4, 1.0
	v_fmac_f32_e32 v4, v5, v4
	v_div_scale_f32 v5, vcc, 1.0, v2, 1.0
	v_mul_f32_e32 v22, v5, v4
	v_fma_f32 v23, -v3, v22, v5
	v_fmac_f32_e32 v22, v23, v4
	v_fma_f32 v3, -v3, v22, v5
	v_div_fmas_f32 v3, v3, v4, v22
	v_div_fixup_f32 v22, v3, v2, 1.0
	v_lshlrev_b64 v[2:3], 11, v[74:75]
	v_lshl_add_u64 v[2:3], s[10:11], 0, v[2:3]
	v_lshl_add_u64 v[2:3], v[72:73], 1, v[2:3]
	v_pk_mul_f32 v[6:7], v[6:7], v[22:23] op_sel_hi:[1,0]
	v_pk_mul_f32 v[8:9], v[8:9], v[22:23] op_sel_hi:[1,0]
	v_lshl_add_u64 v[4:5], v[2:3], 0, v[70:71]
	v_cvt_pk_bf16_f32 v6, v6, v7
	v_cvt_pk_bf16_f32 v7, v8, v9
	global_store_dwordx2 v[4:5], v[6:7], off offset:1024
	v_pk_mul_f32 v[6:7], v[10:11], v[22:23] op_sel_hi:[1,0]
	v_pk_mul_f32 v[8:9], v[12:13], v[22:23] op_sel_hi:[1,0]
	v_cvt_pk_bf16_f32 v6, v6, v7
	v_cvt_pk_bf16_f32 v7, v8, v9
	global_store_dwordx2 v[4:5], v[6:7], off offset:1056
	v_pk_mul_f32 v[6:7], v[18:19], v[22:23] op_sel_hi:[1,0]
	v_pk_mul_f32 v[8:9], v[20:21], v[22:23] op_sel_hi:[1,0]
	v_cvt_pk_bf16_f32 v6, v6, v7
	v_cvt_pk_bf16_f32 v7, v8, v9
	v_lshl_add_u64 v[2:3], v[4:5], 0, s[12:13]
	global_store_dwordx2 v[4:5], v[6:7], off offset:1088
	v_pk_mul_f32 v[4:5], v[14:15], v[22:23] op_sel_hi:[1,0]
	v_pk_mul_f32 v[6:7], v[16:17], v[22:23] op_sel_hi:[1,0]
	v_cvt_pk_bf16_f32 v4, v4, v5

; #define LAS __attribute__((address_space(3)))
; template <bool LOCAL>
; __device__ __forceinline__ void na_unit(const bf16* P, const bf16* VT, bf16* YCAT, const LAS float* rpb_l, LAS bf16* buf, int b, int gr, int hp, int qblk, int tid) {
;     typedef pg8::bf16x8 bf16x8;
;     constexpr int NCH = LOCAL ? 12 : 4, NLOC = LOCAL ? 8 : 0;
;     const int lane = tid & 63, wv = tid >> 6, fr = lane & 15, fq = lane >> 4, hh = wv >> 2, qb = wv & 3, h = 2 * hp + hh;
;     const int qrow0 = LOCAL ? NCTX + b * SEQ + gr * 64 + 16 * qb : b * CTXL + qblk * 64 + 16 * qb;
;     const int r0 = min(max(gr - 4, 0), 24);
;     const int kc0 = qb == 0 ? 0 : qb == 1 ? 8 : qb == 2 ? 24 : 32;
;     const int qcol = 16 * qb + fr, cs = min(max(qcol - 8, 0), 48);
;     const LAS float* rpb = rpb_l + h * 15 * 31;
;     v4u ld[2][2];
;     const int lrow = (tid >> 3) & 63, lseg = tid & 7;
;     ...
;     bf16x8 qf[2];
; #pragma unroll
;     for (int ks = 0; ks < 2; ++ks) qf[ks] = *(const bf16x8*)(P + (size_t)(qrow0 + fr) * DINP + h * 64 + 32 * ks + 8 * fq);
;     f32x4 sl[16], sc[16];
;     float m = -1.0e30f, lsum = 0.f;
;     f32x4 o[4];
; #pragma unroll
;     for (int dt = 0; dt < 4; ++dt) o[dt] = (f32x4){0.f, 0.f, 0.f, 0.f};
;     NA_ISSUE(0); NA_ISSUE(1); NA_STORE(0);
;     __syncthreads();
; #pragma unroll
;     for (int sidx = 0; sidx < 2 * NCH; ++sidx) {
;         if (sidx + 2 < 2 * NCH) NA_ISSUE(sidx + 2);
;         const LAS bf16* cb = buf + (sidx & 1) * 9216 + hh * 4608;
;         if (sidx < NCH) {
;             const int c = sidx;
;             if (LOCAL && c < 8) {
; #pragma unroll
;                 for (int t2 = 0; t2 < 2; ++t2) {
;                     const LAS bf16* kp = cb + (kc0 + 16 * t2 + fr) * 72 + 8 * fq;
;                     f32x4 acc = {0.f, 0.f, 0.f, 0.f};
;                     acc = __builtin_amdgcn_mfma_f32_16x16x32_bf16(*(const LAS bf16x8*)(kp), qf[0], acc, 0, 0, 0);
;                     acc = __builtin_amdgcn_mfma_f32_16x16x32_bf16(*(const LAS bf16x8*)(kp + 32), qf[1], acc, 0, 0, 0);
;                     const LAS float* rb = rpb + (r0 + c - gr + 7) * 31 + 15 - qcol;
; #pragma unroll
;                     for (int e = 0; e < 4; ++e) { const int kcol = kc0 + 16 * t2 + 4 * fq + e; const bool ok = (kcol >= cs) && (kcol < cs + 16);
;                         const float sv = ok ? acc[e] * 0.125f + rb[ok ? kcol : qcol] : -1.0e30f; acc[e] = sv; m = fmaxf(m, sv); }
.LBB0_3992:
	v_mov_b32_e32 v92, v0
	s_mov_b64 s[0:1], -1
	v_and_b32_e32 v88, 15, v92
	v_bfe_u32 v90, v92, 4, 2
	v_ashrrev_i32_e32 v91, 8, v92
	s_cmpk_gt_i32 s69, 0x7ff
	v_bfe_u32 v87, v92, 3, 6
	v_lshlrev_b32_e32 v76, 3, v90
	v_lshlrev_b32_e32 v70, 4, v90
	v_mad_i32_i24 v85, v91, s65, 0
	v_mul_u32_u24_e32 v86, 0x90, v88
	s_waitcnt lgkmcnt(0)
	s_barrier
	s_cbranch_scc0 .LBB0_3994
	s_lshl_b32 s0, s69, 4
	s_and_b32 s0, s0, 0xffffff00
	s_addk_i32 s0, 0x8000
	v_mov_b64_e32 v[78:79], s[8:9]
	s_lshl_b32 s1, s69, 5
	v_or_b32_e32 v77, s0, v87
	v_lshlrev_b32_e32 v4, 4, v92
	s_and_b32 s16, s1, 0x180
	v_mad_u64_u32 v[2:3], s[14:15], v77, s57, v[78:79]
	v_and_b32_e32 v80, 0x70, v4
	v_mov_b32_e32 v81, v71
	v_lshl_add_u64 v[2:3], v[2:3], 0, v[80:81]
	s_lshl_b32 s2, s16, 1
	v_lshl_add_u64 v[2:3], v[2:3], 0, s[2:3]
	global_load_dwordx4 v[6:9], v[2:3], off offset:1024
	global_load_dwordx4 v[10:13], v[2:3], off offset:1152
	s_lshl_b32 s1, s69, 6
	s_and_b32 s1, s1, 0xc0
	v_lshrrev_b32_e32 v2, 2, v92
	v_and_or_b32 v2, v2, 48, s1
	v_lshl_add_u32 v4, v91, 6, s16
	v_or3_b32 v72, v2, v88, s0
	v_ashrrev_i32_e32 v5, 31, v4
	v_mad_u64_u32 v[2:3], s[14:15], v72, s57, v[78:79]
	v_lshlrev_b64 v[74:75], 1, v[4:5]
	v_lshl_add_u64 v[2:3], v[2:3], 0, v[74:75]
	v_or_b32_e32 v14, 64, v77
	v_lshl_add_u64 v[22:23], v[2:3], 0, v[70:71]
	v_mad_u64_u32 v[14:15], s[14:15], v14, s57, v[78:79]
	global_load_dwordx4 v[2:5], v[22:23], off
	v_lshl_add_u64 v[14:15], v[14:15], 0, v[80:81]
	v_lshl_add_u64 v[18:19], v[14:15], 0, s[2:3]
	s_mov_b32 s100, 0x60000
	s_mov_b32 s101, 0
	v_lshl_add_u64 v[248:249], v[18:19], 0, s[100:101]
	global_load_dwordx4 v[14:17], v[18:19], off offset:1024
	s_nop 0
	global_load_dwordx4 v[18:21], v[18:19], off offset:1152
	global_load_dword v250, v[248:249], off offset:1024
	global_load_dword v251, v[248:249], off offset:1152
	s_nop 0
	global_load_dwordx4 v[50:53], v[22:23], off offset:64
	v_mul_u32_u24_e32 v22, 0x90, v87
	v_add3_u32 v73, 0, v22, v80
	v_or_b32_e32 v22, 0x80, v77
	v_add3_u32 v89, v85, v70, v86
	s_mov_b32 s1, s3
	v_cmp_lt_i32_e32 vcc, v82, v83
	s_waitcnt vmcnt(7)
	ds_write_b128 v73, v[6:9]
	s_waitcnt vmcnt(6)
	ds_write_b128 v73, v[10:13] offset:9216
	v_mad_u64_u32 v[10:11], s[14:15], v22, s57, v[78:79]
	v_lshl_add_u64 v[10:11], v[10:11], 0, v[80:81]
	v_lshl_add_u64 v[26:27], v[10:11], 0, s[2:3]
	s_waitcnt lgkmcnt(0)
	s_barrier
	ds_read_b128 v[6:9], v89
	ds_read_b128 v[10:13], v89 offset:2304
	v_lshl_add_u64 v[248:249], v[26:27], 0, s[100:101]
	global_load_dwordx4 v[22:25], v[26:27], off offset:1024
	global_load_dwordx4 v[30:33], v[26:27], off offset:1152
	global_load_dword v250, v[248:249], off offset:1024
	global_load_dword v251, v[248:249], off offset:1152
	ds_read_b128 v[26:29], v89 offset:64
	ds_read_b128 v[34:37], v89 offset:4608
	ds_read_b128 v[38:41], v89 offset:2368
	ds_read_b128 v[42:45], v89 offset:4672
	ds_read_b128 v[46:49], v89 offset:6912
	s_waitcnt vmcnt(9) lgkmcnt(6)
	v_mfma_f32_16x16x32_bf16 v[6:9], v[6:9], v[2:5], 0
	ds_read_b128 v[54:57], v89 offset:6976
	s_waitcnt vmcnt(8)
	ds_write_b128 v73, v[14:17] offset:18432
	s_waitcnt vmcnt(7)
	ds_write_b128 v73, v[18:21] offset:27648
	s_waitcnt lgkmcnt(0)
	v_mfma_f32_16x16x32_bf16 v[10:13], v[10:13], v[2:5], 0
	s_barrier
	v_mfma_f32_16x16x32_bf16 v[14:17], v[34:37], v[2:5], 0
	v_mfma_f32_16x16x32_bf16 v[18:21], v[46:49], v[2:5], 0
	ds_read_b128 v[34:37], v89 offset:18432
	ds_read_b128 v[46:49], v89 offset:18496
	ds_read_b128 v[58:61], v89 offset:20736
	ds_read_b128 v[94:97], v89 offset:20800
	s_waitcnt vmcnt(4)
	v_mfma_f32_16x16x32_bf16 v[62:65], v[26:29], v[50:53], v[6:9]
	s_nop 2
	v_or_b32_e32 v6, s16, v87
	s_waitcnt lgkmcnt(1)
	v_mfma_f32_16x16x32_bf16 v[98:101], v[58:61], v[2:5], 0
	ds_read_b128 v[58:61], v89 offset:23040
	ds_read_b128 v[102:105], v89 offset:23104
	v_mul_u32_u24_e32 v8, 0x9000, v6
	v_mov_b32_e32 v7, v71
	v_mfma_f32_16x16x32_bf16 v[66:69], v[38:41], v[50:53], v[10:13]
	v_mov_b32_e32 v9, v71
	s_nop 1
	v_lshl_add_u64 v[10:11], s[4:5], 0, v[80:81]
	v_or_b32_e32 v12, 64, v6
	v_or_b32_e32 v13, 0xc0, v77
	v_lshl_add_u64 v[10:11], s[0:1], 1, v[10:11]
	v_lshlrev_b32_e32 v6, 1, v8
	v_mul_u32_u24_e32 v8, 0x9000, v12
	v_mad_u64_u32 v[12:13], s[0:1], v13, s57, v[78:79]
	v_lshl_add_u64 v[78:79], v[10:11], 0, v[6:7]
	v_lshlrev_b32_e32 v8, 1, v8
	v_lshl_add_u64 v[6:7], v[12:13], 0, v[80:81]
	v_lshl_add_u64 v[80:81], v[10:11], 0, v[8:9]
	v_lshl_add_u64 v[10:11], v[6:7], 0, s[2:3]
	s_waitcnt lgkmcnt(1)
	v_mfma_f32_16x16x32_bf16 v[106:109], v[58:61], v[2:5], 0
	ds_read_b128 v[58:61], v89 offset:25344
	ds_read_b128 v[110:113], v89 offset:25408
	global_load_dwordx4 v[6:9], v[10:11], off offset:1024
	s_nop 0
	global_load_dwordx4 v[10:13], v[10:11], off offset:1152
	v_mul_f32_e32 v38, 0x3e000000, v68
	s_waitcnt lgkmcnt(1)
	v_mfma_f32_16x16x32_bf16 v[114:117], v[58:61], v[2:5], 0
	v_mul_f32_e32 v39, 0x3e000000, v69
	s_waitcnt vmcnt(5)
	ds_write_b128 v73, v[22:25]
	s_waitcnt vmcnt(4)
	ds_write_b128 v73, v[30:33] offset:9216
	v_mfma_f32_16x16x32_bf16 v[58:61], v[42:45], v[50:53], v[14:17]
	s_waitcnt lgkmcnt(0)
	s_barrier
; #define LAS __attribute__((address_space(3)))
; template <bool LOCAL>
; __device__ __forceinline__ void na_unit(const bf16* P, const bf16* VT, bf16* YCAT, const LAS float* rpb_l, LAS bf16* buf, int b, int gr, int hp, int qblk, int tid) {
;     ...
;                 const int cc = c - NLOC;
; #pragma unroll
;                 for (int t4 = 0; t4 < 4; ++t4) {
;                     const LAS bf16* kp = cb + (16 * t4 + fr) * 72 + 8 * fq;
;                     f32x4 acc = {0.f, 0.f, 0.f, 0.f};
;                     acc = __builtin_amdgcn_mfma_f32_16x16x32_bf16(*(const LAS bf16x8*)(kp), qf[0], acc, 0, 0, 0);
;                     acc = __builtin_amdgcn_mfma_f32_16x16x32_bf16(*(const LAS bf16x8*)(kp + 32), qf[1], acc, 0, 0, 0);
; #pragma unroll
;                     for (int e = 0; e < 4; ++e) { acc[e] *= 0.125f; m = fmaxf(m, acc[e]); }
;                     sc[4 * (cc >= 0 ? cc : 0) + t4] = acc; }
;             }
;             if (sidx == NCH - 1) { m = fmaxf(m, __shfl_xor(m, 16)); m = fmaxf(m, __shfl_xor(m, 32)); }
	s_nop 0
	v_mul_f32_e32 v14, 0x3e000000, v62
	v_mul_f32_e32 v15, 0x3e000000, v63
	v_mfma_f32_16x16x32_bf16 v[54:57], v[54:57], v[50:53], v[18:21]
	s_nop 1
	v_mul_f32_e32 v40, 0x3e000000, v58
	v_mul_f32_e32 v41, 0x3e000000, v59
	v_mul_f32_e32 v77, 0x3e000000, v60
	v_mfma_f32_16x16x32_bf16 v[42:45], v[94:97], v[50:53], v[98:101]
	v_mul_f32_e32 v18, 0x3e000000, v64
	v_mul_f32_e32 v19, 0x3e000000, v65
	v_mul_f32_e32 v20, 0x3e000000, v66
	v_max3_f32 v98, v14, s67, v15
	v_mul_f32_e32 v21, 0x3e000000, v67
	v_max3_f32 v18, v98, v18, v19
	v_mfma_f32_16x16x32_bf16 v[34:37], v[34:37], v[2:5], 0
	v_max3_f32 v18, v18, v20, v21
	ds_read_b128 v[14:17], v89
	v_max3_f32 v22, v18, v38, v39
	ds_read_b128 v[18:21], v89 offset:2304
	v_mul_f32_e32 v93, 0x3e000000, v61
	v_max3_f32 v22, v22, v40, v41
	v_mul_f32_e32 v94, 0x3e000000, v54
	v_mul_f32_e32 v95, 0x3e000000, v55
	v_max3_f32 v38, v22, v77, v93
	v_mfma_f32_16x16x32_bf16 v[46:49], v[46:49], v[50:53], v[34:37]
	v_mul_f32_e32 v96, 0x3e000000, v56
	v_mul_f32_e32 v97, 0x3e000000, v57
	v_max3_f32 v38, v38, v94, v95
	ds_read_b128 v[22:25], v89 offset:64
	ds_read_b128 v[30:33], v89 offset:4608
	v_max3_f32 v38, v38, v96, v97
	ds_read_b128 v[94:97], v89 offset:2368
	v_mfma_f32_16x16x32_bf16 v[34:37], v[102:105], v[50:53], v[106:109]
	v_mul_f32_e32 v99, 0x3e000000, v46
	v_mul_f32_e32 v100, 0x3e000000, v47
	v_mul_f32_e32 v101, 0x3e000000, v48
	v_mul_f32_e32 v102, 0x3e000000, v49
	v_max3_f32 v38, v38, v99, v100
	v_mul_f32_e32 v106, 0x3e000000, v42
	v_mul_f32_e32 v107, 0x3e000000, v43
	s_waitcnt lgkmcnt(4)
	v_mfma_f32_16x16x32_bf16 v[14:17], v[14:17], v[2:5], 0
	v_max3_f32 v38, v38, v101, v102
	v_mul_f32_e32 v108, 0x3e000000, v44
	v_mul_f32_e32 v109, 0x3e000000, v45
	s_waitcnt lgkmcnt(3)
	v_mfma_f32_16x16x32_bf16 v[18:21], v[18:21], v[2:5], 0
	ds_read_b128 v[98:101], v89 offset:4672
	s_waitcnt lgkmcnt(2)
	v_mfma_f32_16x16x32_bf16 v[102:105], v[30:33], v[2:5], 0
	v_max3_f32 v30, v38, v106, v107
	v_max3_f32 v30, v30, v108, v109
	v_mfma_f32_16x16x32_bf16 v[26:29], v[110:113], v[50:53], v[114:117]
	v_mul_f32_e32 v110, 0x3e000000, v34
	v_mul_f32_e32 v111, 0x3e000000, v35
	v_mul_f32_e32 v112, 0x3e000000, v36
	v_mul_f32_e32 v113, 0x3e000000, v37
	v_max3_f32 v30, v30, v110, v111
	v_mfma_f32_16x16x32_bf16 v[38:41], v[22:25], v[50:53], v[14:17]
	s_nop 1
	v_mul_f32_e32 v114, 0x3e000000, v26
	v_mul_f32_e32 v115, 0x3e000000, v27
	v_mul_f32_e32 v116, 0x3e000000, v28
	v_max3_f32 v14, v30, v112, v113
	s_waitcnt lgkmcnt(1)
	v_mfma_f32_16x16x32_bf16 v[30:33], v[94:97], v[50:53], v[18:21]
	v_lshl_add_u64 v[248:249], v[78:79], 0, 0
	v_lshl_add_u64 v[238:239], v[80:81], 0, 0
	global_load_dwordx4 v[94:97], v[78:79], off
	global_load_dwordx4 v[106:109], v[80:81], off
	global_load_dword v250, v[248:249], off offset:128
	global_load_dword v251, v[238:239], off offset:128
	v_mul_f32_e32 v117, 0x3e000000, v29
	v_max3_f32 v14, v14, v114, v115
	v_max3_f32 v22, v14, v116, v117
	ds_read_b128 v[14:17], v89 offset:6912
	v_mul_f32_e32 v23, 0x3e000000, v38
	v_mul_f32_e32 v24, 0x3e000000, v39
	v_mul_f32_e32 v25, 0x3e000000, v40
	v_mul_f32_e32 v77, 0x3e000000, v41
	v_max3_f32 v22, v22, v23, v24
	s_waitcnt lgkmcnt(1)
	v_mfma_f32_16x16x32_bf16 v[18:21], v[98:101], v[50:53], v[102:105]
	v_mul_f32_e32 v93, 0x3e000000, v30
	v_mul_f32_e32 v98, 0x3e000000, v31
	v_max3_f32 v22, v22, v25, v77
	v_max3_f32 v77, v22, v93, v98
	ds_read_b128 v[22:25], v89 offset:6976
	s_waitcnt vmcnt(5)
	ds_write_b128 v73, v[6:9] offset:18432
	s_waitcnt vmcnt(4)
	ds_write_b128 v73, v[10:13] offset:27648
	s_waitcnt lgkmcnt(0)
	s_barrier
	ds_read_b128 v[6:9], v89 offset:18432
	v_mul_f32_e32 v99, 0x3e000000, v32
	v_mul_f32_e32 v10, 0x3e000000, v33
	v_mfma_f32_16x16x32_bf16 v[14:17], v[14:17], v[2:5], 0
	v_max3_f32 v77, v77, v99, v10
	ds_read_b128 v[10:13], v89 offset:18496
	v_mul_f32_e32 v93, 0x3e000000, v18
	v_mfma_f32_16x16x32_bf16 v[22:25], v[22:25], v[50:53], v[14:17]
	v_mul_f32_e32 v98, 0x3e000000, v21
	ds_read_b128 v[110:113], v89 offset:25408
	s_nop 1
	v_mul_f32_e32 v14, 0x3e000000, v19
	v_max3_f32 v77, v77, v93, v14
	s_waitcnt lgkmcnt(2)
	v_mfma_f32_16x16x32_bf16 v[6:9], v[6:9], v[2:5], 0
	ds_read_b128 v[14:17], v89 offset:20736
	v_mul_f32_e32 v93, 0x3e000000, v20
	v_max3_f32 v77, v77, v93, v98
	s_waitcnt lgkmcnt(2)
	v_mfma_f32_16x16x32_bf16 v[10:13], v[10:13], v[50:53], v[6:9]
	v_mul_f32_e32 v93, 0x3e000000, v22
	v_mul_f32_e32 v98, 0x3e000000, v23
	v_max3_f32 v77, v77, v93, v98
	ds_read_b128 v[6:9], v89 offset:20800
	s_waitcnt lgkmcnt(1)
	v_mfma_f32_16x16x32_bf16 v[14:17], v[14:17], v[2:5], 0
	ds_read_b128 v[98:101], v89 offset:23040
	v_mul_f32_e32 v93, 0x3e000000, v24
	v_mul_f32_e32 v102, 0x3e000000, v25
	s_waitcnt lgkmcnt(1)
	v_mfma_f32_16x16x32_bf16 v[14:17], v[6:9], v[50:53], v[14:17]
	ds_read_b128 v[6:9], v89 offset:23104
	v_max3_f32 v77, v77, v93, v102
	ds_read_b128 v[102:105], v89 offset:25344
	s_waitcnt lgkmcnt(2)
	v_mfma_f32_16x16x32_bf16 v[98:101], v[98:101], v[2:5], 0
	v_mul_f32_e32 v93, 0x3e000000, v10
	v_mul_f32_e32 v114, 0x3e000000, v11
	v_mul_f32_e32 v115, 0x3e000000, v12
	s_waitcnt lgkmcnt(1)
	v_mfma_f32_16x16x32_bf16 v[6:9], v[6:9], v[50:53], v[98:101]
	v_mul_f32_e32 v116, 0x3e000000, v13
	v_max3_f32 v77, v77, v93, v114
	v_mul_f32_e32 v117, 0x3e000000, v14
	v_mul_f32_e32 v118, 0x3e000000, v15
	s_waitcnt lgkmcnt(0)
	v_mfma_f32_16x16x32_bf16 v[2:5], v[102:105], v[2:5], 0
	v_max3_f32 v77, v77, v115, v116
	v_mul_f32_e32 v89, 0x3e000000, v16
	v_mul_f32_e32 v98, 0x3e000000, v17
	v_max3_f32 v77, v77, v117, v118
	v_mul_f32_e32 v99, 0x3e000000, v6
	v_mul_f32_e32 v100, 0x3e000000, v7
	v_max3_f32 v77, v77, v89, v98
	v_mul_f32_e32 v101, 0x3e000000, v8
	v_mul_f32_e32 v102, 0x3e000000, v9
	v_max3_f32 v77, v77, v99, v100
	v_mfma_f32_16x16x32_bf16 v[2:5], v[110:113], v[50:53], v[2:5]
	v_max3_f32 v77, v77, v101, v102
	v_lshl_add_u64 v[248:249], v[78:79], 0, 0
	v_lshl_add_u64 v[238:239], v[80:81], 0, 0
	global_load_dwordx4 v[98:101], v[78:79], off offset:128
	global_load_dwordx4 v[102:105], v[80:81], off offset:128
	global_load_dword v250, v[248:249], off offset:256
	global_load_dword v251, v[238:239], off offset:256
	s_waitcnt vmcnt(7)
	ds_write_b128 v73, v[94:97]
	s_waitcnt vmcnt(6)
	ds_write_b128 v73, v[106:109] offset:9216
	s_nop 0
	v_mul_f32_e32 v50, 0x3e000000, v2
	v_mul_f32_e32 v51, 0x3e000000, v3
	v_mul_f32_e32 v52, 0x3e000000, v4
	v_mul_f32_e32 v53, 0x3e000000, v5
	v_max3_f32 v50, v77, v50, v51
	v_max3_f32 v51, v50, v52, v53
	v_cndmask_b32_e32 v50, v1, v82, vcc
	v_lshlrev_b32_e32 v50, 2, v50
	ds_bpermute_b32 v52, v50, v51
	v_cmp_lt_i32_e32 vcc, v84, v83
	s_waitcnt lgkmcnt(0)
	s_barrier
; #define LAS __attribute__((address_space(3)))
; __device__ __forceinline__ unsigned cvt_pk_bf16(float lo, float hi) { const float __attribute__((ext_vector_type(2))) v = {lo, hi}; return __builtin_bit_cast(unsigned, __builtin_convertvector(v, bf16x2_t)); }
; #define NA_STORE(sidx) do { LAS bf16* d_ = buf + ((sidx) & 1) * 9216; _Pragma("unroll") for (int q_ = 0; q_ < 2; ++q_) *(LAS v4u*)(d_ + q_ * 4608 + lrow * 72 + lseg * 8) = ld[(sidx) & 1][q_]; } while (0)
; template <bool LOCAL>
; __device__ __forceinline__ void na_unit(const bf16* P, const bf16* VT, bf16* YCAT, const LAS float* rpb_l, LAS bf16* buf, int b, int gr, int hp, int qblk, int tid) {
;     ...
;             if (sidx == NCH - 1) { m = fmaxf(m, __shfl_xor(m, 16)); m = fmaxf(m, __shfl_xor(m, 32)); }
;     ...
;                 const int cc = c - NLOC;
; #pragma unroll
;                 for (int p2 = 0; p2 < 2; ++p2) {
;                     float p[8];
; #pragma unroll
;                     for (int e = 0; e < 4; ++e) { p[e] = __expf(sc[4 * (cc >= 0 ? cc : 0) + 2 * p2][e] - m); p[4 + e] = __expf(sc[4 * (cc >= 0 ? cc : 0) + 2 * p2 + 1][e] - m); }
; #pragma unroll
;                     for (int e = 0; e < 8; ++e) lsum += p[e];
;                     const bf16x8 pf = __builtin_bit_cast(bf16x8, (v4u){pg8::cvt_pk_bf16(p[0], p[1]), pg8::cvt_pk_bf16(p[2], p[3]), pg8::cvt_pk_bf16(p[4], p[5]), pg8::cvt_pk_bf16(p[6], p[7])});
; #pragma unroll
;                     for (int dt = 0; dt < 4; ++dt) { const LAS bf16* vp = cb + (16 * dt + fr) * 72 + 32 * p2 + 4 * fq;
;                         o[dt] = __builtin_amdgcn_mfma_f32_16x16x32_bf16(frag44(vp, vp + 16), pf, o[dt], 0, 0, 0); }
;                 }
;             }
;         }
;         if (sidx + 1 < 2 * NCH) NA_STORE(sidx + 1);
	v_max_f32_e32 v52, v52, v52
	v_max_f32_e32 v52, v51, v52
	v_cndmask_b32_e32 v51, v1, v84, vcc
	v_lshlrev_b32_e32 v51, 2, v51
	ds_bpermute_b32 v53, v51, v52
	s_waitcnt lgkmcnt(0)
	v_max_f32_e32 v53, v53, v53
	v_max_f32_e32 v77, v52, v53
	v_fma_f32 v52, v62, s66, -v77
	v_fma_f32 v64, v64, s66, -v77
	v_mul_f32_e32 v52, 0x3fb8aa3b, v52
	v_fma_f32 v62, v63, s66, -v77
	v_mul_f32_e32 v64, 0x3fb8aa3b, v64
	v_fma_f32 v65, v65, s66, -v77
	v_exp_f32_e32 v53, v52
	v_fma_f32 v52, v66, s66, -v77
	v_mul_f32_e32 v62, 0x3fb8aa3b, v62
	v_exp_f32_e32 v66, v64
	v_fma_f32 v64, v68, s66, -v77
	v_mul_f32_e32 v65, 0x3fb8aa3b, v65
	v_add3_u32 v68, v85, v76, v86
	v_exp_f32_e32 v63, v62
	v_fma_f32 v62, v67, s66, -v77
	v_exp_f32_e32 v67, v65
	v_fma_f32 v65, v69, s66, -v77
	v_add_u32_e32 v69, 0x800, v68
	v_add_u32_e32 v89, 0x1000, v68
	v_add_u32_e32 v93, 0x1800, v68
	ds_read2_b64 v[94:97], v68 offset1:4
	ds_read2_b64 v[110:113], v69 offset0:32 offset1:36
	ds_read2_b64 v[114:117], v89 offset0:64 offset1:68
	ds_read2_b64 v[118:121], v93 offset0:96 offset1:100
	v_mul_f32_e32 v52, 0x3fb8aa3b, v52
	v_mul_f32_e32 v62, 0x3fb8aa3b, v62
	v_mul_f32_e32 v64, 0x3fb8aa3b, v64
	v_mul_f32_e32 v65, 0x3fb8aa3b, v65
	v_exp_f32_e32 v52, v52
	v_exp_f32_e32 v62, v62
	v_exp_f32_e32 v64, v64
	v_exp_f32_e32 v65, v65
	v_cvt_pk_bf16_f32 v106, v53, v63
	v_cvt_pk_bf16_f32 v107, v66, v67
	v_cvt_pk_bf16_f32 v108, v52, v62
	v_cvt_pk_bf16_f32 v109, v64, v65
	v_fma_f32 v58, v58, s66, -v77
	v_fma_f32 v54, v54, s66, -v77
	s_waitcnt lgkmcnt(3)
	v_mfma_f32_16x16x32_bf16 v[94:97], v[94:97], v[106:109], 0
	v_fma_f32 v59, v59, s66, -v77
	v_fma_f32 v55, v55, s66, -v77
	v_fma_f32 v60, v60, s66, -v77
	s_waitcnt lgkmcnt(2)
	v_mfma_f32_16x16x32_bf16 v[110:113], v[110:113], v[106:109], 0
	v_fma_f32 v56, v56, s66, -v77
	v_fma_f32 v61, v61, s66, -v77
	v_fma_f32 v57, v57, s66, -v77
	s_waitcnt lgkmcnt(1)
	v_mfma_f32_16x16x32_bf16 v[114:117], v[114:117], v[106:109], 0
	v_mul_f32_e32 v58, 0x3fb8aa3b, v58
	v_mul_f32_e32 v54, 0x3fb8aa3b, v54
	v_mul_f32_e32 v59, 0x3fb8aa3b, v59
	s_waitcnt lgkmcnt(0)
	v_mfma_f32_16x16x32_bf16 v[106:109], v[118:121], v[106:109], 0
	ds_read2_b64 v[118:121], v68 offset0:8 offset1:12
	v_mul_f32_e32 v55, 0x3fb8aa3b, v55
	v_mul_f32_e32 v60, 0x3fb8aa3b, v60
	v_mul_f32_e32 v56, 0x3fb8aa3b, v56
	v_mul_f32_e32 v61, 0x3fb8aa3b, v61
	v_mul_f32_e32 v57, 0x3fb8aa3b, v57
	v_exp_f32_e32 v58, v58
	v_exp_f32_e32 v54, v54
	v_exp_f32_e32 v59, v59
	v_exp_f32_e32 v55, v55
	v_exp_f32_e32 v60, v60
	v_exp_f32_e32 v56, v56
	v_exp_f32_e32 v61, v61
	v_exp_f32_e32 v57, v57
	v_cvt_pk_bf16_f32 v122, v58, v59
	v_cvt_pk_bf16_f32 v124, v54, v55
	v_cvt_pk_bf16_f32 v123, v60, v61
	v_cvt_pk_bf16_f32 v125, v56, v57
	v_fma_f32 v42, v42, s66, -v77
	v_mul_f32_e32 v42, 0x3fb8aa3b, v42
	s_waitcnt lgkmcnt(0)
	v_mfma_f32_16x16x32_bf16 v[94:97], v[118:121], v[122:125], v[94:97]
	ds_read2_b64 v[118:121], v69 offset0:40 offset1:44
	v_fma_f32 v46, v46, s66, -v77
	v_mul_f32_e32 v46, 0x3fb8aa3b, v46
	s_waitcnt lgkmcnt(0)
	v_mfma_f32_16x16x32_bf16 v[110:113], v[118:121], v[122:125], v[110:113]
	ds_read2_b64 v[118:121], v89 offset0:72 offset1:76
	v_add_u32_e32 v135, 0x5000, v68
	v_fma_f32 v26, v26, s66, -v77
	s_waitcnt lgkmcnt(0)
	v_mfma_f32_16x16x32_bf16 v[114:117], v[118:121], v[122:125], v[114:117]
	ds_read2_b64 v[118:121], v93 offset0:104 offset1:108
	v_lshl_add_u64 v[248:249], v[78:79], 0, 0
	v_lshl_add_u64 v[238:239], v[80:81], 0, 0
	global_load_dwordx4 v[126:129], v[78:79], off offset:256
	global_load_dwordx4 v[130:133], v[80:81], off offset:256
	global_load_dword v250, v[248:249], off offset:384
	global_load_dword v251, v[238:239], off offset:384
	s_waitcnt vmcnt(7)
	ds_write_b128 v73, v[98:101] offset:18432
	s_waitcnt vmcnt(6)
	ds_write_b128 v73, v[102:105] offset:27648
	s_waitcnt lgkmcnt(2)
	v_mfma_f32_16x16x32_bf16 v[106:109], v[118:121], v[122:125], v[106:109]
	v_exp_f32_e32 v119, v42
	v_fma_f32 v42, v47, s66, -v77
	v_mul_f32_e32 v42, 0x3fb8aa3b, v42
	v_exp_f32_e32 v120, v42
	v_fma_f32 v42, v43, s66, -v77
	v_mul_f32_e32 v42, 0x3fb8aa3b, v42
	v_exp_f32_e32 v121, v42
	v_fma_f32 v42, v48, s66, -v77
	v_mul_f32_e32 v42, 0x3fb8aa3b, v42
	v_exp_f32_e32 v122, v42
	v_fma_f32 v42, v44, s66, -v77
	v_mul_f32_e32 v42, 0x3fb8aa3b, v42
	v_add_u32_e32 v124, 0x4800, v68
	s_waitcnt lgkmcnt(0)
	s_barrier
; #define LAS __attribute__((address_space(3)))
; __device__ __forceinline__ unsigned cvt_pk_bf16(float lo, float hi) { const float __attribute__((ext_vector_type(2))) v = {lo, hi}; return __builtin_bit_cast(unsigned, __builtin_convertvector(v, bf16x2_t)); }
; #define NA_STORE(sidx) do { LAS bf16* d_ = buf + ((sidx) & 1) * 9216; _Pragma("unroll") for (int q_ = 0; q_ < 2; ++q_) *(LAS v4u*)(d_ + q_ * 4608 + lrow * 72 + lseg * 8) = ld[(sidx) & 1][q_]; } while (0)
; template <bool LOCAL>
; __device__ __forceinline__ void na_unit(const bf16* P, const bf16* VT, bf16* YCAT, const LAS float* rpb_l, LAS bf16* buf, int b, int gr, int hp, int qblk, int tid) {
;     ...
;                 const int cc = c - NLOC;
; #pragma unroll
;                 for (int p2 = 0; p2 < 2; ++p2) {
;                     float p[8];
; #pragma unroll
;                     for (int e = 0; e < 4; ++e) { p[e] = __expf(sc[4 * (cc >= 0 ? cc : 0) + 2 * p2][e] - m); p[4 + e] = __expf(sc[4 * (cc >= 0 ? cc : 0) + 2 * p2 + 1][e] - m); }
; #pragma unroll
;                     for (int e = 0; e < 8; ++e) lsum += p[e];
;                     const bf16x8 pf = __builtin_bit_cast(bf16x8, (v4u){pg8::cvt_pk_bf16(p[0], p[1]), pg8::cvt_pk_bf16(p[2], p[3]), pg8::cvt_pk_bf16(p[4], p[5]), pg8::cvt_pk_bf16(p[6], p[7])});
; #pragma unroll
;                     for (int dt = 0; dt < 4; ++dt) { const LAS bf16* vp = cb + (16 * dt + fr) * 72 + 32 * p2 + 4 * fq;
;                         o[dt] = __builtin_amdgcn_mfma_f32_16x16x32_bf16(frag44(vp, vp + 16), pf, o[dt], 0, 0, 0); }
;                 }
;             }
;         }
;         if (sidx + 1 < 2 * NCH) NA_STORE(sidx + 1);
	v_exp_f32_e32 v118, v46
	v_exp_f32_e32 v123, v42
	v_fma_f32 v42, v49, s66, -v77
	ds_read2_b64 v[46:49], v124 offset1:4
	v_mul_f32_e32 v42, 0x3fb8aa3b, v42
	v_exp_f32_e32 v125, v42
	v_fma_f32 v42, v45, s66, -v77
	v_mul_f32_e32 v42, 0x3fb8aa3b, v42
	v_exp_f32_e32 v134, v42
	v_cvt_pk_bf16_f32 v42, v118, v120
	v_cvt_pk_bf16_f32 v43, v122, v125
	v_cvt_pk_bf16_f32 v44, v119, v121
	v_cvt_pk_bf16_f32 v45, v123, v134
	v_mul_f32_e32 v26, 0x3fb8aa3b, v26
	v_fma_f32 v34, v34, s66, -v77
	s_waitcnt lgkmcnt(0)
	v_mfma_f32_16x16x32_bf16 v[46:49], v[46:49], v[42:45], v[94:97]
	v_mul_f32_e32 v34, 0x3fb8aa3b, v34
	v_fma_f32 v30, v30, s66, -v77
	v_mul_f32_e32 v30, 0x3fb8aa3b, v30
	ds_read2_b64 v[94:97], v135 offset0:32 offset1:36
	s_waitcnt lgkmcnt(0)
	v_mfma_f32_16x16x32_bf16 v[94:97], v[94:97], v[42:45], v[110:113]
	s_nop 2
	v_add_u32_e32 v110, 0x5800, v68
	v_add_u32_e32 v111, 0x6000, v68
	ds_read2_b64 v[98:101], v110 offset0:64 offset1:68
	ds_read2_b64 v[102:105], v111 offset0:96 offset1:100
	s_waitcnt lgkmcnt(1)
	v_mfma_f32_16x16x32_bf16 v[98:101], v[98:101], v[42:45], v[114:117]
	v_fma_f32 v38, v38, s66, -v77
	v_mul_f32_e32 v38, 0x3fb8aa3b, v38
	v_fma_f32 v18, v18, s66, -v77
	s_waitcnt lgkmcnt(0)
	v_mfma_f32_16x16x32_bf16 v[42:45], v[102:105], v[42:45], v[106:109]
	v_mul_f32_e32 v18, 0x3fb8aa3b, v18
	v_fma_f32 v10, v10, s66, -v77
	v_mul_f32_e32 v10, 0x3fb8aa3b, v10
	v_exp_f32_e32 v107, v26
	v_fma_f32 v26, v35, s66, -v77
	v_mul_f32_e32 v26, 0x3fb8aa3b, v26
	v_exp_f32_e32 v108, v26
	v_fma_f32 v26, v27, s66, -v77
	v_mul_f32_e32 v26, 0x3fb8aa3b, v26
	v_exp_f32_e32 v109, v26
	v_fma_f32 v26, v36, s66, -v77
	v_mul_f32_e32 v26, 0x3fb8aa3b, v26
	v_exp_f32_e32 v112, v26
	v_fma_f32 v26, v28, s66, -v77
	v_mul_f32_e32 v26, 0x3fb8aa3b, v26
	v_exp_f32_e32 v106, v34
	v_exp_f32_e32 v113, v26
	v_fma_f32 v26, v37, s66, -v77
	ds_read2_b64 v[34:37], v124 offset0:8 offset1:12
	v_mul_f32_e32 v26, 0x3fb8aa3b, v26
	v_exp_f32_e32 v114, v26
	v_fma_f32 v26, v29, s66, -v77
	v_mul_f32_e32 v26, 0x3fb8aa3b, v26
	v_exp_f32_e32 v115, v26
	v_cvt_pk_bf16_f32 v26, v106, v108
	v_cvt_pk_bf16_f32 v27, v112, v114
	v_cvt_pk_bf16_f32 v28, v107, v109
	v_cvt_pk_bf16_f32 v29, v113, v115
	v_fma_f32 v2, v2, s66, -v77
	v_mul_f32_e32 v2, 0x3fb8aa3b, v2
	s_waitcnt lgkmcnt(0)
	v_mfma_f32_16x16x32_bf16 v[34:37], v[34:37], v[26:29], v[46:49]
	v_fma_f32 v6, v6, s66, -v77
	v_mul_f32_e32 v6, 0x3fb8aa3b, v6
	s_nop 0
	ds_read2_b64 v[46:49], v135 offset0:40 offset1:44
	s_waitcnt lgkmcnt(0)
	v_mfma_f32_16x16x32_bf16 v[46:49], v[46:49], v[26:29], v[94:97]
	s_nop 2
	ds_read2_b64 v[94:97], v110 offset0:72 offset1:76
	s_waitcnt lgkmcnt(0)
	v_mfma_f32_16x16x32_bf16 v[94:97], v[94:97], v[26:29], v[98:101]
	s_nop 2
	ds_read2_b64 v[98:101], v111 offset0:104 offset1:108
	global_load_dwordx4 v[102:105], v[78:79], off offset:384
	s_nop 0
	global_load_dwordx4 v[78:81], v[80:81], off offset:384
	s_waitcnt vmcnt(5)
	ds_write_b128 v73, v[126:129]
	s_waitcnt vmcnt(4)
	ds_write_b128 v73, v[130:133] offset:9216
	s_waitcnt lgkmcnt(2)
	v_mfma_f32_16x16x32_bf16 v[26:29], v[98:101], v[26:29], v[42:45]
	v_exp_f32_e32 v99, v30
	v_fma_f32 v30, v39, s66, -v77
	v_mul_f32_e32 v30, 0x3fb8aa3b, v30
	v_exp_f32_e32 v100, v30
	v_fma_f32 v30, v31, s66, -v77
	v_mul_f32_e32 v30, 0x3fb8aa3b, v30
	v_exp_f32_e32 v101, v30
	v_fma_f32 v30, v40, s66, -v77
	v_mul_f32_e32 v30, 0x3fb8aa3b, v30
	v_exp_f32_e32 v116, v30
	v_fma_f32 v30, v32, s66, -v77
	v_mul_f32_e32 v30, 0x3fb8aa3b, v30
	s_waitcnt lgkmcnt(0)
	s_barrier
	v_exp_f32_e32 v98, v38
	v_exp_f32_e32 v117, v30
	v_fma_f32 v30, v41, s66, -v77
	ds_read2_b64 v[38:41], v68 offset1:4
	v_mul_f32_e32 v30, 0x3fb8aa3b, v30
	v_exp_f32_e32 v126, v30
	v_fma_f32 v30, v33, s66, -v77
	v_mul_f32_e32 v30, 0x3fb8aa3b, v30
	v_exp_f32_e32 v127, v30
	v_cvt_pk_bf16_f32 v30, v98, v100
	v_cvt_pk_bf16_f32 v31, v116, v126
	v_cvt_pk_bf16_f32 v32, v99, v101
	v_cvt_pk_bf16_f32 v33, v117, v127
	ds_read2_b64 v[42:45], v89 offset0:64 offset1:68
	s_waitcnt lgkmcnt(1)
	v_mfma_f32_16x16x32_bf16 v[34:37], v[38:41], v[30:33], v[34:37]
	ds_read2_b64 v[38:41], v69 offset0:32 offset1:36
	s_waitcnt lgkmcnt(0)
	v_mfma_f32_16x16x32_bf16 v[38:41], v[38:41], v[30:33], v[46:49]
	s_nop 2
	ds_read2_b64 v[46:49], v93 offset0:96 offset1:100
	s_waitcnt lgkmcnt(0)
	v_mfma_f32_16x16x32_bf16 v[26:29], v[46:49], v[30:33], v[26:29]
	v_exp_f32_e32 v46, v18
	v_fma_f32 v18, v22, s66, -v77
	v_mul_f32_e32 v18, 0x3fb8aa3b, v18
	v_exp_f32_e32 v47, v18
	v_fma_f32 v18, v19, s66, -v77
	v_mul_f32_e32 v18, 0x3fb8aa3b, v18
	v_exp_f32_e32 v48, v18
	v_fma_f32 v18, v23, s66, -v77
	v_mul_f32_e32 v18, 0x3fb8aa3b, v18
	v_exp_f32_e32 v49, v18
	v_fma_f32 v18, v20, s66, -v77
	v_mul_f32_e32 v18, 0x3fb8aa3b, v18
	v_mfma_f32_16x16x32_bf16 v[42:45], v[42:45], v[30:33], v[94:97]
	ds_read2_b64 v[30:33], v69 offset0:40 offset1:44
	s_nop 1
	v_exp_f32_e32 v94, v18
	v_fma_f32 v18, v24, s66, -v77
	v_mul_f32_e32 v18, 0x3fb8aa3b, v18
	v_exp_f32_e32 v95, v18
	v_fma_f32 v18, v21, s66, -v77
	v_mul_f32_e32 v22, 0x3fb8aa3b, v18
	ds_read2_b64 v[18:21], v68 offset0:8 offset1:12
	v_exp_f32_e32 v68, v22
	v_fma_f32 v22, v25, s66, -v77
	v_mul_f32_e32 v22, 0x3fb8aa3b, v22
	v_exp_f32_e32 v96, v22
	v_cvt_pk_bf16_f32 v22, v46, v48
	v_cvt_pk_bf16_f32 v23, v94, v68
	v_cvt_pk_bf16_f32 v24, v47, v49
	v_cvt_pk_bf16_f32 v25, v95, v96
	s_waitcnt lgkmcnt(0)
	s_nop 0
	v_mfma_f32_16x16x32_bf16 v[18:21], v[18:21], v[22:25], v[34:37]
	v_mfma_f32_16x16x32_bf16 v[30:33], v[30:33], v[22:25], v[38:41]
	s_nop 1
	ds_read2_b64 v[34:37], v89 offset0:72 offset1:76
	ds_read2_b64 v[38:41], v93 offset0:104 offset1:108
	s_waitcnt lgkmcnt(1)
	v_mfma_f32_16x16x32_bf16 v[34:37], v[34:37], v[22:25], v[42:45]
	s_waitcnt vmcnt(1)
	ds_write_b128 v73, v[102:105] offset:18432
	s_waitcnt vmcnt(0)
	ds_write_b128 v73, v[78:81] offset:27648
	s_waitcnt lgkmcnt(0)
	s_barrier
; #define LAS __attribute__((address_space(3)))
; __device__ __forceinline__ unsigned cvt_pk_bf16(float lo, float hi) { const float __attribute__((ext_vector_type(2))) v = {lo, hi}; return __builtin_bit_cast(unsigned, __builtin_convertvector(v, bf16x2_t)); }
; #define NA_STORE(sidx) do { LAS bf16* d_ = buf + ((sidx) & 1) * 9216; _Pragma("unroll") for (int q_ = 0; q_ < 2; ++q_) *(LAS v4u*)(d_ + q_ * 4608 + lrow * 72 + lseg * 8) = ld[(sidx) & 1][q_]; } while (0)
; template <bool LOCAL>
; __device__ __forceinline__ void na_unit(const bf16* P, const bf16* VT, bf16* YCAT, const LAS float* rpb_l, LAS bf16* buf, int b, int gr, int hp, int qblk, int tid) {
;     ...
;                 const int cc = c - NLOC;
; #pragma unroll
;                 for (int p2 = 0; p2 < 2; ++p2) {
;                     float p[8];
; #pragma unroll
;                     for (int e = 0; e < 4; ++e) { p[e] = __expf(sc[4 * (cc >= 0 ? cc : 0) + 2 * p2][e] - m); p[4 + e] = __expf(sc[4 * (cc >= 0 ? cc : 0) + 2 * p2 + 1][e] - m); }
; #pragma unroll
;                     for (int e = 0; e < 8; ++e) lsum += p[e];
;                     const bf16x8 pf = __builtin_bit_cast(bf16x8, (v4u){pg8::cvt_pk_bf16(p[0], p[1]), pg8::cvt_pk_bf16(p[2], p[3]), pg8::cvt_pk_bf16(p[4], p[5]), pg8::cvt_pk_bf16(p[6], p[7])});
; #pragma unroll
;                     for (int dt = 0; dt < 4; ++dt) { const LAS bf16* vp = cb + (16 * dt + fr) * 72 + 32 * p2 + 4 * fq;
;                         o[dt] = __builtin_amdgcn_mfma_f32_16x16x32_bf16(frag44(vp, vp + 16), pf, o[dt], 0, 0, 0); }
;                 }
;             }
;         }
;         if (sidx + 1 < 2 * NCH) NA_STORE(sidx + 1);
;         __syncthreads();
;     }
;     ...
;     lsum += __shfl_xor(lsum, 16); lsum += __shfl_xor(lsum, 32);
;     const float inv = 1.f / lsum;
;     bf16* op = YCAT + (size_t)(qrow0 + fr) * D + 512 + h * 64 + 4 * fq;
; #pragma unroll
;     for (int dt = 0; dt < 4; ++dt) { v2u w; w.x = pg8::cvt_pk_bf16(o[dt][0] * inv, o[dt][1] * inv); w.y = pg8::cvt_pk_bf16(o[dt][2] * inv, o[dt][3] * inv); *(v2u*)(op + dt * 16) = w; }
	v_mfma_f32_16x16x32_bf16 v[22:25], v[38:41], v[22:25], v[26:29]
	v_exp_f32_e32 v38, v10
	v_fma_f32 v10, v14, s66, -v77
	v_mul_f32_e32 v10, 0x3fb8aa3b, v10
	v_exp_f32_e32 v39, v10
	v_fma_f32 v10, v11, s66, -v77
	v_mul_f32_e32 v10, 0x3fb8aa3b, v10
	v_exp_f32_e32 v40, v10
	v_fma_f32 v10, v15, s66, -v77
	v_mul_f32_e32 v10, 0x3fb8aa3b, v10
	v_exp_f32_e32 v41, v10
	v_fma_f32 v10, v12, s66, -v77
	v_mul_f32_e32 v10, 0x3fb8aa3b, v10
	v_exp_f32_e32 v42, v10
	v_fma_f32 v10, v16, s66, -v77
	v_mul_f32_e32 v10, 0x3fb8aa3b, v10
	v_exp_f32_e32 v43, v10
	v_fma_f32 v10, v13, s66, -v77
	ds_read2_b64 v[26:29], v110 offset0:64 offset1:68
	v_mul_f32_e32 v14, 0x3fb8aa3b, v10
	v_exp_f32_e32 v44, v14
	v_fma_f32 v14, v17, s66, -v77
	v_mul_f32_e32 v14, 0x3fb8aa3b, v14
	v_exp_f32_e32 v45, v14
	v_cvt_pk_bf16_f32 v14, v38, v40
	v_cvt_pk_bf16_f32 v15, v42, v44
	v_cvt_pk_bf16_f32 v16, v39, v41
	v_cvt_pk_bf16_f32 v17, v43, v45
	ds_read2_b64 v[10:13], v124 offset1:4
	v_mov_b32_e32 v73, v71
	s_waitcnt lgkmcnt(1)
	v_mfma_f32_16x16x32_bf16 v[26:29], v[26:29], v[14:17], v[34:37]
	s_nop 2
	v_add_f32_e32 v34, 0, v53
	v_add_f32_e32 v34, v63, v34
	v_add_f32_e32 v34, v66, v34
	v_add_f32_e32 v34, v67, v34
	v_add_f32_e32 v34, v52, v34
	v_add_f32_e32 v34, v62, v34
	v_add_f32_e32 v34, v64, v34
	v_add_f32_e32 v34, v65, v34
	v_add_f32_e32 v34, v58, v34
	v_add_f32_e32 v34, v59, v34
	v_add_f32_e32 v34, v60, v34
	v_add_f32_e32 v34, v61, v34
	v_add_f32_e32 v34, v54, v34
	v_add_f32_e32 v34, v55, v34
	v_add_f32_e32 v34, v56, v34
	v_add_f32_e32 v34, v57, v34
	s_waitcnt lgkmcnt(0)
	v_mfma_f32_16x16x32_bf16 v[10:13], v[10:13], v[14:17], v[18:21]
	v_add_f32_e32 v34, v118, v34
	v_add_f32_e32 v34, v120, v34
	v_add_f32_e32 v34, v122, v34
	ds_read2_b64 v[18:21], v135 offset0:32 offset1:36
	v_add_f32_e32 v34, v125, v34
	v_add_f32_e32 v34, v119, v34
	v_add_f32_e32 v34, v121, v34
	v_add_f32_e32 v34, v123, v34
	v_add_f32_e32 v34, v134, v34
	v_add_f32_e32 v34, v106, v34
	s_waitcnt lgkmcnt(0)
	v_mfma_f32_16x16x32_bf16 v[18:21], v[18:21], v[14:17], v[30:33]
	v_add_f32_e32 v34, v108, v34
	s_nop 1
	ds_read2_b64 v[30:33], v111 offset0:96 offset1:100
	v_add_f32_e32 v34, v112, v34
	v_add_f32_e32 v34, v114, v34
	v_add_f32_e32 v34, v107, v34
	v_add_f32_e32 v34, v109, v34
	v_add_f32_e32 v34, v113, v34
	v_add_f32_e32 v34, v115, v34
	v_add_f32_e32 v34, v98, v34
	v_add_f32_e32 v34, v100, v34
	s_waitcnt lgkmcnt(0)
	v_mfma_f32_16x16x32_bf16 v[14:17], v[30:33], v[14:17], v[22:25]
	v_add_f32_e32 v34, v116, v34
	v_add_f32_e32 v34, v126, v34
	v_add_f32_e32 v34, v99, v34
	v_exp_f32_e32 v23, v2
	v_fma_f32 v2, v7, s66, -v77
	v_mul_f32_e32 v2, 0x3fb8aa3b, v2
	v_exp_f32_e32 v24, v2
	v_fma_f32 v2, v3, s66, -v77
	v_mul_f32_e32 v2, 0x3fb8aa3b, v2
	v_add_f32_e32 v34, v101, v34
	v_exp_f32_e32 v25, v2
	v_fma_f32 v2, v8, s66, -v77
	v_add_f32_e32 v34, v117, v34
	v_mul_f32_e32 v2, 0x3fb8aa3b, v2
	v_add_f32_e32 v34, v127, v34
	v_exp_f32_e32 v30, v2
	v_fma_f32 v2, v4, s66, -v77
	v_add_f32_e32 v34, v46, v34
	v_mul_f32_e32 v2, 0x3fb8aa3b, v2
	v_add_f32_e32 v34, v48, v34
	v_exp_f32_e32 v22, v6
	v_exp_f32_e32 v31, v2
	v_fma_f32 v2, v9, s66, -v77
	ds_read2_b64 v[6:9], v124 offset0:8 offset1:12
	v_add_f32_e32 v34, v94, v34
	v_mul_f32_e32 v2, 0x3fb8aa3b, v2
	v_add_f32_e32 v34, v68, v34
	v_exp_f32_e32 v32, v2
	v_fma_f32 v2, v5, s66, -v77
	v_add_f32_e32 v34, v47, v34
	v_mul_f32_e32 v2, 0x3fb8aa3b, v2
	v_add_f32_e32 v34, v49, v34
	v_exp_f32_e32 v33, v2
	v_add_f32_e32 v34, v95, v34
	v_add_f32_e32 v34, v96, v34
	v_add_f32_e32 v34, v38, v34
	v_add_f32_e32 v34, v40, v34
	v_cvt_pk_bf16_f32 v2, v22, v24
	v_cvt_pk_bf16_f32 v3, v30, v32
	v_cvt_pk_bf16_f32 v4, v23, v25
	v_cvt_pk_bf16_f32 v5, v31, v33
	v_add_f32_e32 v34, v42, v34
	v_add_f32_e32 v34, v44, v34
	s_waitcnt lgkmcnt(0)
	v_mfma_f32_16x16x32_bf16 v[6:9], v[6:9], v[2:5], v[10:13]
	v_add_f32_e32 v34, v39, v34
	v_add_f32_e32 v34, v41, v34
	v_add_f32_e32 v34, v43, v34
	ds_read2_b64 v[10:13], v135 offset0:40 offset1:44
	v_add_f32_e32 v34, v45, v34
	v_add_f32_e32 v22, v22, v34
	v_add_f32_e32 v22, v24, v22
	v_add_f32_e32 v22, v30, v22
	v_add_f32_e32 v22, v32, v22
	s_waitcnt lgkmcnt(0)
	v_mfma_f32_16x16x32_bf16 v[10:13], v[10:13], v[2:5], v[18:21]
	s_nop 2
	ds_read2_b64 v[18:21], v110 offset0:72 offset1:76
	v_add_f32_e32 v22, v23, v22
	v_add_f32_e32 v22, v25, v22
	v_add_f32_e32 v22, v31, v22
	v_add_f32_e32 v30, v33, v22
	ds_bpermute_b32 v31, v50, v30
	ds_read2_b64 v[22:25], v111 offset0:104 offset1:108
	s_waitcnt lgkmcnt(2)
	v_mfma_f32_16x16x32_bf16 v[18:21], v[18:21], v[2:5], v[26:29]
	v_mov_b32_e32 v77, v71
	s_waitcnt lgkmcnt(1)
	s_nop 0
	v_add_f32_e32 v26, v30, v31
	ds_bpermute_b32 v27, v51, v26
	s_waitcnt lgkmcnt(1)
	v_mfma_f32_16x16x32_bf16 v[14:17], v[22:25], v[2:5], v[14:17]
	s_waitcnt lgkmcnt(0)
	v_add_f32_e32 v2, v26, v27
	v_div_scale_f32 v3, s[0:1], v2, v2, 1.0
	v_rcp_f32_e32 v4, v3
	s_barrier
	s_mov_b64 s[0:1], 0
	v_fma_f32 v5, -v3, v4, 1.0
	v_fmac_f32_e32 v4, v5, v4
	v_div_scale_f32 v5, vcc, 1.0, v2, 1.0
	v_mul_f32_e32 v22, v5, v4
	v_fma_f32 v23, -v3, v22, v5
	v_fmac_f32_e32 v22, v23, v4
	v_fma_f32 v3, -v3, v22, v5
	v_div_fmas_f32 v3, v3, v4, v22
	v_div_fixup_f32 v22, v3, v2, 1.0
	v_lshlrev_b64 v[2:3], 11, v[72:73]
	v_lshl_add_u64 v[2:3], s[10:11], 0, v[2:3]
	v_lshl_add_u64 v[2:3], v[2:3], 0, v[74:75]
	v_pk_mul_f32 v[6:7], v[6:7], v[22:23] op_sel_hi:[1,0]
	v_pk_mul_f32 v[8:9], v[8:9], v[22:23] op_sel_hi:[1,0]
	v_lshl_add_u64 v[4:5], v[2:3], 0, v[76:77]
	v_cvt_pk_bf16_f32 v6, v6, v7
	v_cvt_pk_bf16_f32 v7, v8, v9
	global_store_dwordx2 v[4:5], v[6:7], off offset:1024
	v_pk_mul_f32 v[6:7], v[10:11], v[22:23] op_sel_hi:[1,0]
	v_pk_mul_f32 v[8:9], v[12:13], v[22:23] op_sel_hi:[1,0]
	v_cvt_pk_bf16_f32 v6, v6, v7
	v_cvt_pk_bf16_f32 v7, v8, v9
	global_store_dwordx2 v[4:5], v[6:7], off offset:1056
	v_pk_mul_f32 v[6:7], v[18:19], v[22:23] op_sel_hi:[1,0]
	v_pk_mul_f32 v[8:9], v[20:21], v[22:23] op_sel_hi:[1,0]
	v_cvt_pk_bf16_f32 v6, v6, v7
	v_cvt_pk_bf16_f32 v7, v8, v9
	v_lshl_add_u64 v[2:3], v[4:5], 0, s[12:13]
	global_store_dwordx2 v[4:5], v[6:7], off offset:1088
	v_pk_mul_f32 v[4:5], v[14:15], v[22:23] op_sel_hi:[1,0]
	v_pk_mul_f32 v[6:7], v[16:17], v[22:23] op_sel_hi:[1,0]
	v_cvt_pk_bf16_f32 v4, v4, v5

; #define LAS __attribute__((address_space(3)))
; template <bool LOCAL>
; __device__ __forceinline__ void na_unit(const bf16* P, const bf16* VT, bf16* YCAT, const LAS float* rpb_l, LAS bf16* buf, int b, int gr, int hp, int qblk, int tid) {
;     typedef pg8::bf16x8 bf16x8;
;     constexpr int NCH = LOCAL ? 12 : 4, NLOC = LOCAL ? 8 : 0;
;     const int lane = tid & 63, wv = tid >> 6, fr = lane & 15, fq = lane >> 4, hh = wv >> 2, qb = wv & 3, h = 2 * hp + hh;
;     const int qrow0 = LOCAL ? NCTX + b * SEQ + gr * 64 + 16 * qb : b * CTXL + qblk * 64 + 16 * qb;
;     const int r0 = min(max(gr - 4, 0), 24);
;     const int kc0 = qb == 0 ? 0 : qb == 1 ? 8 : qb == 2 ? 24 : 32;
;     const int qcol = 16 * qb + fr, cs = min(max(qcol - 8, 0), 48);
;     const LAS float* rpb = rpb_l + h * 15 * 31;
;     v4u ld[2][2];
;     const int lrow = (tid >> 3) & 63, lseg = tid & 7;
;     ...
;     bf16x8 qf[2];
; #pragma unroll
;     for (int ks = 0; ks < 2; ++ks) qf[ks] = *(const bf16x8*)(P + (size_t)(qrow0 + fr) * DINP + h * 64 + 32 * ks + 8 * fq);
;     f32x4 sl[16], sc[16];
;     float m = -1.0e30f, lsum = 0.f;
;     f32x4 o[4];
; #pragma unroll
;     for (int dt = 0; dt < 4; ++dt) o[dt] = (f32x4){0.f, 0.f, 0.f, 0.f};
;     NA_ISSUE(0); NA_ISSUE(1); NA_STORE(0);
;     __syncthreads();
; #pragma unroll
;     for (int sidx = 0; sidx < 2 * NCH; ++sidx) {
;         if (sidx + 2 < 2 * NCH) NA_ISSUE(sidx + 2);
;         const LAS bf16* cb = buf + (sidx & 1) * 9216 + hh * 4608;
;         if (sidx < NCH) {
;             const int c = sidx;
;             if (LOCAL && c < 8) {
; #pragma unroll
;                 for (int t2 = 0; t2 < 2; ++t2) {
;                     const LAS bf16* kp = cb + (kc0 + 16 * t2 + fr) * 72 + 8 * fq;
;                     f32x4 acc = {0.f, 0.f, 0.f, 0.f};
;                     acc = __builtin_amdgcn_mfma_f32_16x16x32_bf16(*(const LAS bf16x8*)(kp), qf[0], acc, 0, 0, 0);
;                     acc = __builtin_amdgcn_mfma_f32_16x16x32_bf16(*(const LAS bf16x8*)(kp + 32), qf[1], acc, 0, 0, 0);
;                     const LAS float* rb = rpb + (r0 + c - gr + 7) * 31 + 15 - qcol;
; #pragma unroll
;                     for (int e = 0; e < 4; ++e) { const int kcol = kc0 + 16 * t2 + 4 * fq + e; const bool ok = (kcol >= cs) && (kcol < cs + 16);
;                         const float sv = ok ? acc[e] * 0.125f + rb[ok ? kcol : qcol] : -1.0e30f; acc[e] = sv; m = fmaxf(m, sv); }
.LBB0_4001:
	s_or_b64 exec, exec, s[0:1]
	s_bfe_u32 s19, s69, 0x50002
	v_sub_u32_e64 v3, s19, 4 clamp
	s_ashr_i32 s17, s69, 7
	v_readfirstlane_b32 s0, v3
	s_lshl_b32 s26, s17, 11
	s_min_u32 s20, s0, 24
	s_add_i32 s14, s26, 0x1000
	s_lshl_b32 s15, s20, 6
	s_or_b32 s16, s15, s14
	v_mov_b64_e32 v[18:19], s[8:9]
	v_and_b32_e32 v32, 7, v92
	v_or_b32_e32 v3, s16, v87
	s_and_b32 s18, s69, 3
	v_mad_i64_i32 v[4:5], s[0:1], v3, s57, v[18:19]
	v_lshlrev_b32_e32 v26, 4, v32
	v_mov_b32_e32 v27, v71
	v_lshl_add_u64 v[4:5], v[4:5], 0, v[26:27]
	s_lshl_b32 s2, s18, 8
	v_lshl_add_u64 v[4:5], v[4:5], 0, s[2:3]
	global_load_dwordx4 v[10:13], v[4:5], off offset:1024
	global_load_dwordx4 v[14:17], v[4:5], off offset:1152
	s_lshl_b32 s0, s19, 6
	v_lshl_or_b32 v31, v2, 4, v88
	v_lshl_add_u32 v34, s18, 1, v91
	s_or_b32 s0, s14, s0
	v_mad_u32_u24 v2, v87, s64, 0
	v_lshlrev_b32_e32 v72, 6, v34
	s_add_i32 s50, s26, 0x1040
	v_or_b32_e32 v74, s0, v31
	v_add_u32_e32 v75, v2, v26
	v_ashrrev_i32_e32 v73, 31, v72
	v_or_b32_e32 v4, s50, v87
	v_mad_i64_i32 v[2:3], s[0:1], v74, s57, v[18:19]
	v_add_u32_e32 v4, s15, v4
	v_lshl_add_u64 v[2:3], v[72:73], 1, v[2:3]
	v_mad_i64_i32 v[4:5], s[0:1], v4, s57, v[18:19]
	v_lshl_add_u64 v[2:3], v[2:3], 0, v[70:71]
	v_lshl_add_u64 v[20:21], v[4:5], 0, v[26:27]
	global_load_dwordx4 v[6:9], v[2:3], off
	s_nop 0
	global_load_dwordx4 v[2:5], v[2:3], off offset:64
	s_or_b32 s14, s26, s15
	s_addk_i32 s14, 0x1080
	v_or_b32_e32 v24, s14, v87
	v_mad_i64_i32 v[28:29], s[0:1], v24, s57, v[18:19]
	v_lshl_add_u64 v[26:27], v[28:29], 0, v[26:27]
	v_lshl_add_u64 v[22:23], v[20:21], 0, s[2:3]
	v_lshl_add_u64 v[26:27], v[26:27], 0, s[2:3]
	s_mov_b32 s100, 0x60000
	s_mov_b32 s101, 0
	v_lshl_add_u64 v[248:249], v[22:23], 0, s[100:101]
	global_load_dwordx4 v[18:21], v[22:23], off offset:1024
	s_nop 0
	global_load_dwordx4 v[22:25], v[22:23], off offset:1152
	global_load_dword v250, v[248:249], off offset:1024
	global_load_dword v251, v[248:249], off offset:1152
	v_add_u32_e32 v30, v85, v70
	v_add_u32_e32 v33, v89, v88
	v_mad_u32_u24 v36, v33, s64, v30
	s_sub_i32 s0, s20, s19
	s_mulk_i32 s0, 0x7c
	v_sub_u32_e64 v35, v31, 8 clamp
	v_mul_lo_u32 v34, v34, s68
	s_add_i32 s0, s0, 0
	v_min_u32_e32 v35, 48, v35
	v_lshlrev_b32_e32 v77, 2, v90
	v_add_u32_e32 v34, s0, v34
	v_lshlrev_b32_e32 v31, 2, v31
	v_sub_u32_e32 v31, v34, v31
	v_add_u32_e32 v34, v89, v77
	v_cmp_ge_u32_e32 vcc, v34, v35
	v_mov_b32_e32 v90, 0xf149f2ca
	v_lshl_add_u32 v31, v34, 2, v31
	v_mov_b32_e32 v91, 0xf149f2ca
	s_waitcnt vmcnt(7)
	ds_write_b128 v75, v[10:13]
	s_waitcnt vmcnt(6)
	ds_write_b128 v75, v[14:17] offset:9216
	s_waitcnt lgkmcnt(0)
	s_barrier
	ds_read_b32 v240, v31 offset:37792
	ds_read_b32 v241, v31 offset:37796
	ds_read_b32 v242, v31 offset:37800
	ds_read_b32 v243, v31 offset:37804
	ds_read_b32 v244, v31 offset:37856
	ds_read_b32 v245, v31 offset:37860
	ds_read_b32 v246, v31 offset:37864
	ds_read_b32 v247, v31 offset:37868
	v_lshl_add_u64 v[248:249], v[26:27], 0, s[100:101]
	global_load_dwordx4 v[10:13], v[26:27], off offset:1024
	global_load_dwordx4 v[14:17], v[26:27], off offset:1152
	global_load_dword v250, v[248:249], off offset:1024
	global_load_dword v251, v[248:249], off offset:1152
	ds_read_b128 v[26:29], v36
	ds_read_b128 v[38:41], v36 offset:64
	s_waitcnt vmcnt(9) lgkmcnt(1)
	v_mfma_f32_16x16x32_bf16 v[26:29], v[26:29], v[6:9], 0
	v_add_u32_e32 v36, 16, v35
	v_cmp_lt_u32_e64 s[0:1], v34, v36
	s_and_b64 s[28:29], vcc, s[0:1]
	s_waitcnt vmcnt(8) lgkmcnt(0)
	v_mfma_f32_16x16x32_bf16 v[26:29], v[38:41], v[2:5], v[26:29]
	s_nop 2
	s_waitcnt lgkmcnt(0)
	s_nop 3
	v_fmac_f32_e32 v240, 0x3e000000, v26
	v_cndmask_b32_e64 v91, v91, v240, s[28:29]
	s_nop 4
	v_or_b32_e32 v26, 1, v34
	v_cmp_ge_u32_e32 vcc, v26, v35
	v_cmp_lt_u32_e64 s[0:1], v26, v36
	s_and_b64 s[30:31], vcc, s[0:1]
	s_nop 2
	s_waitcnt lgkmcnt(0)
	v_fmac_f32_e32 v241, 0x3e000000, v27
	v_cndmask_b32_e64 v90, v90, v241, s[30:31]
	v_or_b32_e32 v26, 2, v34
	v_cmp_ge_u32_e32 vcc, v26, v35
	v_cmp_lt_u32_e64 s[0:1], v26, v36
	s_and_b64 s[34:35], vcc, s[0:1]
	v_mov_b32_e32 v92, 0xf149f2ca
	v_mov_b32_e32 v93, 0xf149f2ca
	s_nop 2
	s_waitcnt lgkmcnt(0)
	v_fmac_f32_e32 v242, 0x3e000000, v28
	v_cndmask_b32_e64 v93, v93, v242, s[34:35]
	v_or_b32_e32 v26, 3, v34
	v_cmp_ge_u32_e32 vcc, v26, v35
	v_cmp_lt_u32_e64 s[0:1], v26, v36
	s_and_b64 s[36:37], vcc, s[0:1]
	s_nop 2
	s_waitcnt lgkmcnt(0)
	v_fmac_f32_e32 v243, 0x3e000000, v29
	v_cndmask_b32_e64 v92, v92, v243, s[36:37]
	v_add_u32_e32 v37, 16, v89
	v_add_u32_e32 v34, v37, v88
	v_mad_u32_u24 v38, v34, s64, v30
	ds_read_b128 v[26:29], v38
	ds_read_b128 v[38:41], v38 offset:64
	v_add_u32_e32 v37, v37, v77
	v_cmp_ge_u32_e32 vcc, v37, v35
	v_cmp_lt_u32_e64 s[0:1], v37, v36
	s_waitcnt lgkmcnt(1)
	v_mfma_f32_16x16x32_bf16 v[26:29], v[26:29], v[6:9], 0
	s_and_b64 s[38:39], vcc, s[0:1]
	v_mov_b32_e32 v94, 0xf149f2ca
	v_mov_b32_e32 v95, 0xf149f2ca
	s_waitcnt lgkmcnt(0)
	v_mfma_f32_16x16x32_bf16 v[26:29], v[38:41], v[2:5], v[26:29]
	s_nop 2
	s_waitcnt lgkmcnt(0)
	s_nop 3
	v_fmac_f32_e32 v244, 0x3e000000, v26
	v_cndmask_b32_e64 v95, v95, v244, s[38:39]
	s_nop 4
	v_or_b32_e32 v26, 1, v37
	v_cmp_ge_u32_e32 vcc, v26, v35
	v_cmp_lt_u32_e64 s[0:1], v26, v36
	s_and_b64 s[44:45], vcc, s[0:1]
	s_nop 2
	s_waitcnt lgkmcnt(0)
	v_fmac_f32_e32 v245, 0x3e000000, v27
	v_cndmask_b32_e64 v94, v94, v245, s[44:45]
	v_or_b32_e32 v26, 2, v37
	v_cmp_ge_u32_e32 vcc, v26, v35
	v_cmp_lt_u32_e64 s[0:1], v26, v36
	s_and_b64 s[46:47], vcc, s[0:1]
	v_mov_b32_e32 v98, 0xf149f2ca
	v_mov_b32_e32 v99, 0xf149f2ca
	s_nop 2
	s_waitcnt lgkmcnt(0)
	v_fmac_f32_e32 v246, 0x3e000000, v28
	v_cndmask_b32_e64 v99, v99, v246, s[46:47]
	v_or_b32_e32 v26, 3, v37
	v_cmp_ge_u32_e32 vcc, v26, v35
	v_cmp_lt_u32_e64 s[0:1], v26, v36
	s_and_b64 s[48:49], vcc, s[0:1]
	s_nop 2
	s_waitcnt lgkmcnt(0)
	v_fmac_f32_e32 v247, 0x3e000000, v29
	v_cndmask_b32_e64 v98, v98, v247, s[48:49]
	v_mul_u32_u24_e32 v27, 0x90, v33
	v_lshlrev_b32_e32 v26, 3, v32
	v_add_u32_e32 v32, v30, v27
	s_waitcnt vmcnt(7)
	ds_write_b128 v75, v[18:21] offset:18432
	s_waitcnt vmcnt(6)
	ds_write_b128 v75, v[22:25] offset:27648
	s_waitcnt lgkmcnt(0)
	s_barrier
; #define LAS __attribute__((address_space(3)))
; template <bool LOCAL>
; __device__ __forceinline__ void na_unit(const bf16* P, const bf16* VT, bf16* YCAT, const LAS float* rpb_l, LAS bf16* buf, int b, int gr, int hp, int qblk, int tid) {
;     ...
;     for (int sidx = 0; sidx < 2 * NCH; ++sidx) {
;         if (sidx + 2 < 2 * NCH) NA_ISSUE(sidx + 2);
;         const LAS bf16* cb = buf + (sidx & 1) * 9216 + hh * 4608;
;         if (sidx < NCH) {
;             const int c = sidx;
;             if (LOCAL && c < 8) {
; #pragma unroll
;                 for (int t2 = 0; t2 < 2; ++t2) {
;                     const LAS bf16* kp = cb + (kc0 + 16 * t2 + fr) * 72 + 8 * fq;
;                     f32x4 acc = {0.f, 0.f, 0.f, 0.f};
;                     acc = __builtin_amdgcn_mfma_f32_16x16x32_bf16(*(const LAS bf16x8*)(kp), qf[0], acc, 0, 0, 0);
;                     acc = __builtin_amdgcn_mfma_f32_16x16x32_bf16(*(const LAS bf16x8*)(kp + 32), qf[1], acc, 0, 0, 0);
;                     const LAS float* rb = rpb + (r0 + c - gr + 7) * 31 + 15 - qcol;
; #pragma unroll
;                     for (int e = 0; e < 4; ++e) { const int kcol = kc0 + 16 * t2 + 4 * fq + e; const bool ok = (kcol >= cs) && (kcol < cs + 16);
;                         const float sv = ok ? acc[e] * 0.125f + rb[ok ? kcol : qcol] : -1.0e30f; acc[e] = sv; m = fmaxf(m, sv); }
;                     sl[2 * (c < 8 ? c : 0) + t2] = acc; }
	ds_read_b32 v240, v31 offset:37916
	ds_read_b32 v241, v31 offset:37920
	ds_read_b32 v242, v31 offset:37924
	ds_read_b32 v243, v31 offset:37928
	ds_read_b32 v244, v31 offset:37980
	ds_read_b32 v245, v31 offset:37984
	ds_read_b32 v246, v31 offset:37988
	ds_read_b32 v247, v31 offset:37992
	ds_read_b128 v[18:21], v32 offset:18432
	s_add_i32 s26, s26, s15
	s_add_i32 s0, s26, 0x10c0
	v_or_b32_e32 v24, s0, v87
	v_mov_b64_e32 v[22:23], s[8:9]
	s_lshl_b32 s1, s18, 7
	v_mad_i64_i32 v[22:23], s[18:19], v24, s57, v[22:23]
	v_lshlrev_b32_e32 v70, 1, v26
	v_lshl_add_u64 v[22:23], v[22:23], 0, v[70:71]
	s_lshl_b32 s2, s1, 1
	v_lshl_add_u64 v[22:23], v[22:23], 0, s[2:3]
	ds_read_b128 v[26:29], v32 offset:18496
	s_waitcnt lgkmcnt(1)
	v_mfma_f32_16x16x32_bf16 v[36:39], v[18:21], v[6:9], 0
	v_lshl_add_u64 v[248:249], v[22:23], 0, s[100:101]
	global_load_dwordx4 v[18:21], v[22:23], off offset:1024
	s_nop 0
	global_load_dwordx4 v[22:25], v[22:23], off offset:1152
	global_load_dword v250, v[248:249], off offset:1024
	global_load_dword v251, v[248:249], off offset:1152
	v_mov_b32_e32 v96, 0xf149f2ca
	v_mov_b32_e32 v97, 0xf149f2ca
	s_waitcnt lgkmcnt(0)
	v_mfma_f32_16x16x32_bf16 v[26:29], v[26:29], v[2:5], v[36:39]
	s_nop 2
	s_waitcnt lgkmcnt(0)
	s_nop 3
	v_fmac_f32_e32 v240, 0x3e000000, v26
	v_cndmask_b32_e64 v97, v97, v240, s[28:29]
	s_nop 2
	s_waitcnt lgkmcnt(0)
	s_nop 0
	v_fmac_f32_e32 v241, 0x3e000000, v27
	v_cndmask_b32_e64 v96, v96, v241, s[30:31]
	v_mov_b32_e32 v100, 0xf149f2ca
	v_mov_b32_e32 v101, 0xf149f2ca
	s_nop 2
	s_waitcnt lgkmcnt(0)
	v_fmac_f32_e32 v242, 0x3e000000, v28
	v_cndmask_b32_e64 v101, v101, v242, s[34:35]
	s_nop 2
	s_waitcnt lgkmcnt(0)
	v_fmac_f32_e32 v243, 0x3e000000, v29
	v_cndmask_b32_e64 v100, v100, v243, s[36:37]
	v_mul_u32_u24_e32 v26, 0x90, v34
	v_add_u32_e32 v33, v30, v26
	ds_read_b128 v[26:29], v33 offset:18432
	ds_read_b128 v[34:37], v33 offset:18496
	v_mov_b32_e32 v103, 0xf149f2ca
	v_mov_b32_e32 v105, 0xf149f2ca
	s_waitcnt lgkmcnt(1)
	v_mfma_f32_16x16x32_bf16 v[26:29], v[26:29], v[6:9], 0
	s_waitcnt lgkmcnt(0)
	v_mfma_f32_16x16x32_bf16 v[26:29], v[34:37], v[2:5], v[26:29]
	s_nop 2
	s_waitcnt lgkmcnt(0)
	s_nop 3
	v_fmac_f32_e32 v244, 0x3e000000, v26
	v_cndmask_b32_e64 v105, v105, v244, s[38:39]
	s_nop 2
	s_waitcnt lgkmcnt(0)
	s_nop 0
	v_fmac_f32_e32 v245, 0x3e000000, v27
	v_cndmask_b32_e64 v103, v103, v245, s[44:45]
	v_mov_b32_e32 v107, 0xf149f2ca
	v_mov_b32_e32 v109, 0xf149f2ca
	s_nop 2
	s_waitcnt lgkmcnt(0)
	v_fmac_f32_e32 v246, 0x3e000000, v28
	v_cndmask_b32_e64 v109, v109, v246, s[46:47]
	s_nop 2
	s_waitcnt lgkmcnt(0)
	v_fmac_f32_e32 v247, 0x3e000000, v29
	v_cndmask_b32_e64 v107, v107, v247, s[48:49]
	s_waitcnt vmcnt(7)
	ds_write_b128 v75, v[10:13]
	s_waitcnt vmcnt(6)
	ds_write_b128 v75, v[14:17] offset:9216
	s_waitcnt lgkmcnt(0)
	s_barrier
	ds_read_b32 v240, v31 offset:38040
	ds_read_b32 v241, v31 offset:38044
	ds_read_b32 v242, v31 offset:38048
	ds_read_b32 v243, v31 offset:38052
	ds_read_b32 v244, v31 offset:38104
	ds_read_b32 v245, v31 offset:38108
	ds_read_b32 v246, v31 offset:38112
	ds_read_b32 v247, v31 offset:38116
	ds_read_b128 v[10:13], v32
	ds_read_b128 v[26:29], v32 offset:64
	s_add_i32 s18, s26, 0x1100
	v_or_b32_e32 v16, s18, v87
	v_mov_b64_e32 v[14:15], s[8:9]
	v_mad_i64_i32 v[14:15], s[20:21], v16, s57, v[14:15]
	v_lshl_add_u64 v[14:15], v[14:15], 0, v[70:71]
	v_lshl_add_u64 v[14:15], v[14:15], 0, s[2:3]
	s_waitcnt lgkmcnt(1)
	v_mfma_f32_16x16x32_bf16 v[34:37], v[10:13], v[6:9], 0
	v_lshl_add_u64 v[248:249], v[14:15], 0, s[100:101]
	global_load_dwordx4 v[10:13], v[14:15], off offset:1024
	s_nop 0
	global_load_dwordx4 v[14:17], v[14:15], off offset:1152
	global_load_dword v250, v[248:249], off offset:1024
	global_load_dword v251, v[248:249], off offset:1152
	v_mov_b32_e32 v102, 0xf149f2ca
	v_mov_b32_e32 v104, 0xf149f2ca
	s_waitcnt lgkmcnt(0)
	v_mfma_f32_16x16x32_bf16 v[26:29], v[26:29], v[2:5], v[34:37]
	s_nop 2
	s_waitcnt lgkmcnt(0)
	s_nop 3
	v_fmac_f32_e32 v240, 0x3e000000, v26
	v_cndmask_b32_e64 v104, v104, v240, s[28:29]
	s_nop 2
	s_waitcnt lgkmcnt(0)
	s_nop 0
	v_fmac_f32_e32 v241, 0x3e000000, v27
	v_cndmask_b32_e64 v102, v102, v241, s[30:31]
	v_mov_b32_e32 v106, 0xf149f2ca
	v_mov_b32_e32 v108, 0xf149f2ca
	s_nop 2
	s_waitcnt lgkmcnt(0)
	v_fmac_f32_e32 v242, 0x3e000000, v28
	v_cndmask_b32_e64 v108, v108, v242, s[34:35]
	s_nop 2
	s_waitcnt lgkmcnt(0)
	v_fmac_f32_e32 v243, 0x3e000000, v29
	v_cndmask_b32_e64 v106, v106, v243, s[36:37]
	ds_read_b128 v[26:29], v33
	ds_read_b128 v[34:37], v33 offset:64
	v_mov_b32_e32 v110, 0xf149f2ca
	v_mov_b32_e32 v113, 0xf149f2ca
	s_waitcnt lgkmcnt(1)
	v_mfma_f32_16x16x32_bf16 v[26:29], v[26:29], v[6:9], 0
	s_waitcnt lgkmcnt(0)
	v_mfma_f32_16x16x32_bf16 v[26:29], v[34:37], v[2:5], v[26:29]
	s_nop 2
	s_waitcnt lgkmcnt(0)
	s_nop 3
	v_fmac_f32_e32 v244, 0x3e000000, v26
	v_cndmask_b32_e64 v113, v113, v244, s[38:39]
	s_nop 2
	s_waitcnt lgkmcnt(0)
	s_nop 0
	v_fmac_f32_e32 v245, 0x3e000000, v27
	v_cndmask_b32_e64 v110, v110, v245, s[44:45]
	v_mov_b32_e32 v112, 0xf149f2ca
	v_mov_b32_e32 v116, 0xf149f2ca
	s_nop 2
	s_waitcnt lgkmcnt(0)
	v_fmac_f32_e32 v246, 0x3e000000, v28
	v_cndmask_b32_e64 v116, v116, v246, s[46:47]
	s_nop 2
	s_waitcnt lgkmcnt(0)
	v_fmac_f32_e32 v247, 0x3e000000, v29
	v_cndmask_b32_e64 v112, v112, v247, s[48:49]
	s_waitcnt vmcnt(7)
	ds_write_b128 v75, v[18:21] offset:18432
	s_waitcnt vmcnt(6)
	ds_write_b128 v75, v[22:25] offset:27648
	s_waitcnt lgkmcnt(0)
	s_barrier
; #define LAS __attribute__((address_space(3)))
; template <bool LOCAL>
; __device__ __forceinline__ void na_unit(const bf16* P, const bf16* VT, bf16* YCAT, const LAS float* rpb_l, LAS bf16* buf, int b, int gr, int hp, int qblk, int tid) {
;     ...
;     for (int sidx = 0; sidx < 2 * NCH; ++sidx) {
;         if (sidx + 2 < 2 * NCH) NA_ISSUE(sidx + 2);
;         const LAS bf16* cb = buf + (sidx & 1) * 9216 + hh * 4608;
;         if (sidx < NCH) {
;             const int c = sidx;
;             if (LOCAL && c < 8) {
; #pragma unroll
;                 for (int t2 = 0; t2 < 2; ++t2) {
;                     const LAS bf16* kp = cb + (kc0 + 16 * t2 + fr) * 72 + 8 * fq;
;                     f32x4 acc = {0.f, 0.f, 0.f, 0.f};
;                     acc = __builtin_amdgcn_mfma_f32_16x16x32_bf16(*(const LAS bf16x8*)(kp), qf[0], acc, 0, 0, 0);
;                     acc = __builtin_amdgcn_mfma_f32_16x16x32_bf16(*(const LAS bf16x8*)(kp + 32), qf[1], acc, 0, 0, 0);
;                     const LAS float* rb = rpb + (r0 + c - gr + 7) * 31 + 15 - qcol;
; #pragma unroll
;                     for (int e = 0; e < 4; ++e) { const int kcol = kc0 + 16 * t2 + 4 * fq + e; const bool ok = (kcol >= cs) && (kcol < cs + 16);
;                         const float sv = ok ? acc[e] * 0.125f + rb[ok ? kcol : qcol] : -1.0e30f; acc[e] = sv; m = fmaxf(m, sv); }
;                     sl[2 * (c < 8 ? c : 0) + t2] = acc; }
	ds_read_b32 v240, v31 offset:38164
	ds_read_b32 v241, v31 offset:38168
	ds_read_b32 v242, v31 offset:38172
	ds_read_b32 v243, v31 offset:38176
	ds_read_b32 v244, v31 offset:38228
	ds_read_b32 v245, v31 offset:38232
	ds_read_b32 v246, v31 offset:38236
	ds_read_b32 v247, v31 offset:38240
	ds_read_b128 v[18:21], v32 offset:18432
	ds_read_b128 v[26:29], v32 offset:18496
	s_add_i32 s20, s26, 0x1140
	v_or_b32_e32 v24, s20, v87
	v_mov_b64_e32 v[22:23], s[8:9]
	v_mad_i64_i32 v[22:23], s[22:23], v24, s57, v[22:23]
	v_lshl_add_u64 v[22:23], v[22:23], 0, v[70:71]
	v_lshl_add_u64 v[22:23], v[22:23], 0, s[2:3]
	s_waitcnt lgkmcnt(1)
	v_mfma_f32_16x16x32_bf16 v[34:37], v[18:21], v[6:9], 0
	v_lshl_add_u64 v[248:249], v[22:23], 0, s[100:101]
	global_load_dwordx4 v[18:21], v[22:23], off offset:1024
	s_nop 0
	global_load_dwordx4 v[22:25], v[22:23], off offset:1152
	global_load_dword v250, v[248:249], off offset:1024
	global_load_dword v251, v[248:249], off offset:1152
	v_mov_b32_e32 v111, 0xf149f2ca
	v_mov_b32_e32 v114, 0xf149f2ca
	s_waitcnt lgkmcnt(0)
	v_mfma_f32_16x16x32_bf16 v[26:29], v[26:29], v[2:5], v[34:37]
	s_nop 2
	s_waitcnt lgkmcnt(0)
	s_nop 3
	v_fmac_f32_e32 v240, 0x3e000000, v26
	v_cndmask_b32_e64 v114, v114, v240, s[28:29]
	s_nop 2
	s_waitcnt lgkmcnt(0)
	s_nop 0
	v_fmac_f32_e32 v241, 0x3e000000, v27
	v_cndmask_b32_e64 v111, v111, v241, s[30:31]
	v_mov_b32_e32 v115, 0xf149f2ca
	v_mov_b32_e32 v117, 0xf149f2ca
	s_nop 2
	s_waitcnt lgkmcnt(0)
	v_fmac_f32_e32 v242, 0x3e000000, v28
	v_cndmask_b32_e64 v117, v117, v242, s[34:35]
	s_nop 2
	s_waitcnt lgkmcnt(0)
	v_fmac_f32_e32 v243, 0x3e000000, v29
	v_cndmask_b32_e64 v115, v115, v243, s[36:37]
	ds_read_b128 v[26:29], v33 offset:18432
	ds_read_b128 v[34:37], v33 offset:18496
	v_mov_b32_e32 v118, 0xf149f2ca
	v_mov_b32_e32 v121, 0xf149f2ca
	s_waitcnt lgkmcnt(1)
	v_mfma_f32_16x16x32_bf16 v[26:29], v[26:29], v[6:9], 0
	s_waitcnt lgkmcnt(0)
	v_mfma_f32_16x16x32_bf16 v[26:29], v[34:37], v[2:5], v[26:29]
	s_nop 2
	s_waitcnt lgkmcnt(0)
	s_nop 3
	v_fmac_f32_e32 v244, 0x3e000000, v26
	v_cndmask_b32_e64 v121, v121, v244, s[38:39]
	s_nop 2
	s_waitcnt lgkmcnt(0)
	s_nop 0
	v_fmac_f32_e32 v245, 0x3e000000, v27
	v_cndmask_b32_e64 v118, v118, v245, s[44:45]
	v_mov_b32_e32 v120, 0xf149f2ca
	v_mov_b32_e32 v124, 0xf149f2ca
	s_nop 2
	s_waitcnt lgkmcnt(0)
	v_fmac_f32_e32 v246, 0x3e000000, v28
	v_cndmask_b32_e64 v124, v124, v246, s[46:47]
	s_nop 2
	s_waitcnt lgkmcnt(0)
	v_fmac_f32_e32 v247, 0x3e000000, v29
	v_cndmask_b32_e64 v120, v120, v247, s[48:49]
	s_waitcnt vmcnt(7)
	ds_write_b128 v75, v[10:13]
	s_waitcnt vmcnt(6)
	ds_write_b128 v75, v[14:17] offset:9216
	s_waitcnt lgkmcnt(0)
	s_barrier
	ds_read_b32 v240, v31 offset:38288
	ds_read_b32 v241, v31 offset:38292
	ds_read_b32 v242, v31 offset:38296
	ds_read_b32 v243, v31 offset:38300
	ds_read_b32 v244, v31 offset:38352
	ds_read_b32 v245, v31 offset:38356
	ds_read_b32 v246, v31 offset:38360
	ds_read_b32 v247, v31 offset:38364
	ds_read_b128 v[10:13], v32
	ds_read_b128 v[26:29], v32 offset:64
	s_add_i32 s22, s26, 0x1180
	v_or_b32_e32 v16, s22, v87
	v_mov_b64_e32 v[14:15], s[8:9]
	v_mad_i64_i32 v[14:15], s[24:25], v16, s57, v[14:15]
	v_lshl_add_u64 v[14:15], v[14:15], 0, v[70:71]
	v_lshl_add_u64 v[14:15], v[14:15], 0, s[2:3]
	s_waitcnt lgkmcnt(1)
	v_mfma_f32_16x16x32_bf16 v[34:37], v[10:13], v[6:9], 0
	v_lshl_add_u64 v[248:249], v[14:15], 0, s[100:101]
	global_load_dwordx4 v[10:13], v[14:15], off offset:1024
	s_nop 0
	global_load_dwordx4 v[14:17], v[14:15], off offset:1152
	global_load_dword v250, v[248:249], off offset:1024
	global_load_dword v251, v[248:249], off offset:1152
	v_mov_b32_e32 v119, 0xf149f2ca
	v_mov_b32_e32 v122, 0xf149f2ca
	s_waitcnt lgkmcnt(0)
	v_mfma_f32_16x16x32_bf16 v[26:29], v[26:29], v[2:5], v[34:37]
	s_nop 2
	s_waitcnt lgkmcnt(0)
	s_nop 3
	v_fmac_f32_e32 v240, 0x3e000000, v26
	v_cndmask_b32_e64 v122, v122, v240, s[28:29]
	s_nop 2
	s_waitcnt lgkmcnt(0)
	s_nop 0
	v_fmac_f32_e32 v241, 0x3e000000, v27
	v_cndmask_b32_e64 v119, v119, v241, s[30:31]
	v_mov_b32_e32 v123, 0xf149f2ca
	v_mov_b32_e32 v125, 0xf149f2ca
	s_nop 2
	s_waitcnt lgkmcnt(0)
	v_fmac_f32_e32 v242, 0x3e000000, v28
	v_cndmask_b32_e64 v125, v125, v242, s[34:35]
	s_nop 2
	s_waitcnt lgkmcnt(0)
	v_fmac_f32_e32 v243, 0x3e000000, v29
	v_cndmask_b32_e64 v123, v123, v243, s[36:37]
	ds_read_b128 v[26:29], v33
	ds_read_b128 v[34:37], v33 offset:64
	v_mov_b32_e32 v127, 0xf149f2ca
	v_mov_b32_e32 v130, 0xf149f2ca
	s_waitcnt lgkmcnt(1)
	v_mfma_f32_16x16x32_bf16 v[26:29], v[26:29], v[6:9], 0
	s_waitcnt lgkmcnt(0)
	v_mfma_f32_16x16x32_bf16 v[26:29], v[34:37], v[2:5], v[26:29]
	s_nop 2
	s_waitcnt lgkmcnt(0)
	s_nop 3
	v_fmac_f32_e32 v244, 0x3e000000, v26
	v_cndmask_b32_e64 v130, v130, v244, s[38:39]
	s_nop 2
	s_waitcnt lgkmcnt(0)
	s_nop 0
	v_fmac_f32_e32 v245, 0x3e000000, v27
	v_cndmask_b32_e64 v127, v127, v245, s[44:45]
	v_mov_b32_e32 v129, 0xf149f2ca
	v_mov_b32_e32 v134, 0xf149f2ca
	s_nop 2
	s_waitcnt lgkmcnt(0)
	v_fmac_f32_e32 v246, 0x3e000000, v28
	v_cndmask_b32_e64 v134, v134, v246, s[46:47]
	s_nop 2
	s_waitcnt lgkmcnt(0)
	v_fmac_f32_e32 v247, 0x3e000000, v29
	v_cndmask_b32_e64 v129, v129, v247, s[48:49]
	s_waitcnt vmcnt(7)
	ds_write_b128 v75, v[18:21] offset:18432
	s_waitcnt vmcnt(6)
	ds_write_b128 v75, v[22:25] offset:27648
	s_waitcnt lgkmcnt(0)
	s_barrier
; #define LAS __attribute__((address_space(3)))
; template <bool LOCAL>
; __device__ __forceinline__ void na_unit(const bf16* P, const bf16* VT, bf16* YCAT, const LAS float* rpb_l, LAS bf16* buf, int b, int gr, int hp, int qblk, int tid) {
;     ...
;     for (int sidx = 0; sidx < 2 * NCH; ++sidx) {
;         if (sidx + 2 < 2 * NCH) NA_ISSUE(sidx + 2);
;         const LAS bf16* cb = buf + (sidx & 1) * 9216 + hh * 4608;
;         if (sidx < NCH) {
;             const int c = sidx;
;             if (LOCAL && c < 8) {
; #pragma unroll
;                 for (int t2 = 0; t2 < 2; ++t2) {
;                     const LAS bf16* kp = cb + (kc0 + 16 * t2 + fr) * 72 + 8 * fq;
;                     f32x4 acc = {0.f, 0.f, 0.f, 0.f};
;                     acc = __builtin_amdgcn_mfma_f32_16x16x32_bf16(*(const LAS bf16x8*)(kp), qf[0], acc, 0, 0, 0);
;                     acc = __builtin_amdgcn_mfma_f32_16x16x32_bf16(*(const LAS bf16x8*)(kp + 32), qf[1], acc, 0, 0, 0);
;                     const LAS float* rb = rpb + (r0 + c - gr + 7) * 31 + 15 - qcol;
; #pragma unroll
;                     for (int e = 0; e < 4; ++e) { const int kcol = kc0 + 16 * t2 + 4 * fq + e; const bool ok = (kcol >= cs) && (kcol < cs + 16);
;                         const float sv = ok ? acc[e] * 0.125f + rb[ok ? kcol : qcol] : -1.0e30f; acc[e] = sv; m = fmaxf(m, sv); }
;                     sl[2 * (c < 8 ? c : 0) + t2] = acc; }
	ds_read_b32 v240, v31 offset:38412
	ds_read_b32 v241, v31 offset:38416
	ds_read_b32 v242, v31 offset:38420
	ds_read_b32 v243, v31 offset:38424
	ds_read_b32 v244, v31 offset:38476
	ds_read_b32 v245, v31 offset:38480
	ds_read_b32 v246, v31 offset:38484
	ds_read_b32 v247, v31 offset:38488
	ds_read_b128 v[18:21], v32 offset:18432
	ds_read_b128 v[26:29], v32 offset:18496
	s_add_i32 s24, s26, 0x11c0
	v_or_b32_e32 v24, s24, v87
	v_mov_b64_e32 v[22:23], s[8:9]
	v_mad_i64_i32 v[22:23], s[26:27], v24, s57, v[22:23]
	v_lshl_add_u64 v[22:23], v[22:23], 0, v[70:71]
	v_lshl_add_u64 v[22:23], v[22:23], 0, s[2:3]
	s_waitcnt lgkmcnt(1)
	v_mfma_f32_16x16x32_bf16 v[34:37], v[18:21], v[6:9], 0
	global_load_dwordx4 v[18:21], v[22:23], off offset:1024
	s_nop 0
	global_load_dwordx4 v[22:25], v[22:23], off offset:1152
	v_mov_b32_e32 v128, 0xf149f2ca
	v_mov_b32_e32 v131, 0xf149f2ca
	s_waitcnt lgkmcnt(0)
	v_mfma_f32_16x16x32_bf16 v[26:29], v[26:29], v[2:5], v[34:37]
	s_nop 2
	s_waitcnt lgkmcnt(0)
	s_nop 3
	v_fmac_f32_e32 v240, 0x3e000000, v26
	v_cndmask_b32_e64 v131, v131, v240, s[28:29]
	s_nop 2
	s_waitcnt lgkmcnt(0)
	s_nop 0
	v_fmac_f32_e32 v241, 0x3e000000, v27
	v_cndmask_b32_e64 v128, v128, v241, s[30:31]
	v_mov_b32_e32 v133, 0xf149f2ca
	v_mov_b32_e32 v135, 0xf149f2ca
	s_nop 2
	s_waitcnt lgkmcnt(0)
	v_fmac_f32_e32 v242, 0x3e000000, v28
	v_cndmask_b32_e64 v135, v135, v242, s[34:35]
	s_nop 2
	s_waitcnt lgkmcnt(0)
	v_fmac_f32_e32 v243, 0x3e000000, v29
	v_cndmask_b32_e64 v133, v133, v243, s[36:37]
	ds_read_b128 v[26:29], v33 offset:18432
	ds_read_b128 v[34:37], v33 offset:18496
	v_mov_b32_e32 v136, 0xf149f2ca
	v_mov_b32_e32 v139, 0xf149f2ca
	s_waitcnt lgkmcnt(1)
	v_mfma_f32_16x16x32_bf16 v[26:29], v[26:29], v[6:9], 0
	s_waitcnt lgkmcnt(0)
	v_mfma_f32_16x16x32_bf16 v[26:29], v[34:37], v[2:5], v[26:29]
	s_nop 2
	s_waitcnt lgkmcnt(0)
	s_nop 3
	v_fmac_f32_e32 v244, 0x3e000000, v26
	v_cndmask_b32_e64 v139, v139, v244, s[38:39]
	s_nop 2
	s_waitcnt lgkmcnt(0)
	s_nop 0
	v_fmac_f32_e32 v245, 0x3e000000, v27
	v_cndmask_b32_e64 v136, v136, v245, s[44:45]
	v_mov_b32_e32 v138, 0xf149f2ca
	v_mov_b32_e32 v142, 0xf149f2ca
	s_nop 2
	s_waitcnt lgkmcnt(0)
	v_fmac_f32_e32 v246, 0x3e000000, v28
	v_cndmask_b32_e64 v142, v142, v246, s[46:47]
	s_nop 2
	s_waitcnt lgkmcnt(0)
	v_fmac_f32_e32 v247, 0x3e000000, v29
	v_cndmask_b32_e64 v138, v138, v247, s[48:49]
	s_waitcnt vmcnt(5)
	ds_write_b128 v75, v[10:13]
	s_waitcnt vmcnt(4)
	ds_write_b128 v75, v[14:17] offset:9216
	s_waitcnt lgkmcnt(0)
	s_barrier
	ds_read_b32 v240, v31 offset:38536
	ds_read_b32 v241, v31 offset:38540
	ds_read_b32 v242, v31 offset:38544
	ds_read_b32 v243, v31 offset:38548
	ds_read_b32 v244, v31 offset:38600
	ds_read_b32 v245, v31 offset:38604
	ds_read_b32 v246, v31 offset:38608
	ds_read_b32 v247, v31 offset:38612
	ds_read_b128 v[10:13], v32
	ds_read_b128 v[26:29], v32 offset:64
	s_lshl_b32 s26, s17, 8
	v_or_b32_e32 v34, s26, v87
	v_mov_b64_e32 v[14:15], s[8:9]
	v_mad_i64_i32 v[14:15], s[52:53], v34, s57, v[14:15]
	v_lshl_add_u64 v[14:15], v[14:15], 0, v[70:71]
	v_lshl_add_u64 v[14:15], v[14:15], 0, s[2:3]
	s_waitcnt lgkmcnt(1)
	v_mfma_f32_16x16x32_bf16 v[36:39], v[10:13], v[6:9], 0
	v_lshl_add_u64 v[248:249], v[14:15], 0, s[100:101]
	global_load_dwordx4 v[10:13], v[14:15], off offset:1024
	s_nop 0
	global_load_dwordx4 v[14:17], v[14:15], off offset:1152
	global_load_dword v250, v[248:249], off offset:1024
	global_load_dword v251, v[248:249], off offset:1152
	v_mov_b32_e32 v137, 0xf149f2ca
	v_mov_b32_e32 v140, 0xf149f2ca
	s_waitcnt lgkmcnt(0)
	v_mfma_f32_16x16x32_bf16 v[26:29], v[26:29], v[2:5], v[36:39]
	s_nop 2
	s_waitcnt lgkmcnt(0)
	s_nop 3
	v_fmac_f32_e32 v240, 0x3e000000, v26
	v_cndmask_b32_e64 v140, v140, v240, s[28:29]
	s_nop 2
	s_waitcnt lgkmcnt(0)
	s_nop 0
	v_fmac_f32_e32 v241, 0x3e000000, v27
	v_cndmask_b32_e64 v137, v137, v241, s[30:31]
	v_mov_b32_e32 v141, 0xf149f2ca
	v_mov_b32_e32 v143, 0xf149f2ca
	s_nop 2
	s_waitcnt lgkmcnt(0)
	v_fmac_f32_e32 v242, 0x3e000000, v28
	v_cndmask_b32_e64 v143, v143, v242, s[34:35]
	s_nop 2
	s_waitcnt lgkmcnt(0)
	v_fmac_f32_e32 v243, 0x3e000000, v29
	v_cndmask_b32_e64 v141, v141, v243, s[36:37]
	ds_read_b128 v[26:29], v33
	ds_read_b128 v[36:39], v33 offset:64
	v_mov_b32_e32 v144, 0xf149f2ca
	v_mov_b32_e32 v147, 0xf149f2ca
	s_waitcnt lgkmcnt(1)
	v_mfma_f32_16x16x32_bf16 v[26:29], v[26:29], v[6:9], 0
	s_waitcnt lgkmcnt(0)
	v_mfma_f32_16x16x32_bf16 v[26:29], v[36:39], v[2:5], v[26:29]
	s_nop 2
	s_waitcnt lgkmcnt(0)
	s_nop 3
	v_fmac_f32_e32 v244, 0x3e000000, v26
	v_cndmask_b32_e64 v147, v147, v244, s[38:39]
	s_nop 2
	s_waitcnt lgkmcnt(0)
	s_nop 0
	v_fmac_f32_e32 v245, 0x3e000000, v27
	v_cndmask_b32_e64 v144, v144, v245, s[44:45]
	v_mov_b32_e32 v146, 0xf149f2ca
	v_mov_b32_e32 v150, 0xf149f2ca
	s_nop 2
	s_waitcnt lgkmcnt(0)
	v_fmac_f32_e32 v246, 0x3e000000, v28
	v_cndmask_b32_e64 v150, v150, v246, s[46:47]
	s_nop 2
	s_waitcnt lgkmcnt(0)
	v_fmac_f32_e32 v247, 0x3e000000, v29
	v_cndmask_b32_e64 v146, v146, v247, s[48:49]
	s_waitcnt vmcnt(5)
	ds_write_b128 v75, v[18:21] offset:18432
	s_waitcnt vmcnt(4)
	ds_write_b128 v75, v[22:25] offset:27648
	s_waitcnt lgkmcnt(0)
	s_barrier
; #define LAS __attribute__((address_space(3)))
; template <bool LOCAL>
; __device__ __forceinline__ void na_unit(const bf16* P, const bf16* VT, bf16* YCAT, const LAS float* rpb_l, LAS bf16* buf, int b, int gr, int hp, int qblk, int tid) {
;     ...
;         if (sidx < NCH) {
;             const int c = sidx;
;             if (LOCAL && c < 8) {
; #pragma unroll
;                 for (int t2 = 0; t2 < 2; ++t2) {
;                     const LAS bf16* kp = cb + (kc0 + 16 * t2 + fr) * 72 + 8 * fq;
;                     f32x4 acc = {0.f, 0.f, 0.f, 0.f};
;                     acc = __builtin_amdgcn_mfma_f32_16x16x32_bf16(*(const LAS bf16x8*)(kp), qf[0], acc, 0, 0, 0);
;                     acc = __builtin_amdgcn_mfma_f32_16x16x32_bf16(*(const LAS bf16x8*)(kp + 32), qf[1], acc, 0, 0, 0);
;                     const LAS float* rb = rpb + (r0 + c - gr + 7) * 31 + 15 - qcol;
; #pragma unroll
;                     for (int e = 0; e < 4; ++e) { const int kcol = kc0 + 16 * t2 + 4 * fq + e; const bool ok = (kcol >= cs) && (kcol < cs + 16);
;                         const float sv = ok ? acc[e] * 0.125f + rb[ok ? kcol : qcol] : -1.0e30f; acc[e] = sv; m = fmaxf(m, sv); }
;                     sl[2 * (c < 8 ? c : 0) + t2] = acc; }
;             } else {
;                 const int cc = c - NLOC;
; #pragma unroll
;                 for (int t4 = 0; t4 < 4; ++t4) {
;                     const LAS bf16* kp = cb + (16 * t4 + fr) * 72 + 8 * fq;
;                     f32x4 acc = {0.f, 0.f, 0.f, 0.f};
;                     acc = __builtin_amdgcn_mfma_f32_16x16x32_bf16(*(const LAS bf16x8*)(kp), qf[0], acc, 0, 0, 0);
;                     acc = __builtin_amdgcn_mfma_f32_16x16x32_bf16(*(const LAS bf16x8*)(kp + 32), qf[1], acc, 0, 0, 0);
; #pragma unroll
;                     for (int e = 0; e < 4; ++e) { acc[e] *= 0.125f; m = fmaxf(m, acc[e]); }
;                     sc[4 * (cc >= 0 ? cc : 0) + t4] = acc; }
;             }
;             if (sidx == NCH - 1) { m = fmaxf(m, __shfl_xor(m, 16)); m = fmaxf(m, __shfl_xor(m, 32)); }
	ds_read_b32 v240, v31 offset:38660
	ds_read_b32 v241, v31 offset:38664
	ds_read_b32 v242, v31 offset:38668
	ds_read_b32 v243, v31 offset:38672
	ds_read_b32 v244, v31 offset:38724
	ds_read_b32 v245, v31 offset:38728
	ds_read_b32 v246, v31 offset:38732
	ds_read_b32 v247, v31 offset:38736
	ds_read_b128 v[18:21], v32 offset:18432
	ds_read_b128 v[26:29], v32 offset:18496
	v_or_b32_e32 v24, 64, v34
	v_mov_b64_e32 v[22:23], s[8:9]
	v_mad_i64_i32 v[22:23], s[52:53], v24, s57, v[22:23]
	v_lshl_add_u64 v[22:23], v[22:23], 0, v[70:71]
	v_lshl_add_u64 v[22:23], v[22:23], 0, s[2:3]
	s_waitcnt lgkmcnt(1)
	v_mfma_f32_16x16x32_bf16 v[36:39], v[18:21], v[6:9], 0
	v_lshl_add_u64 v[248:249], v[22:23], 0, s[100:101]
	global_load_dwordx4 v[18:21], v[22:23], off offset:1024
	s_nop 0
	global_load_dwordx4 v[22:25], v[22:23], off offset:1152
	global_load_dword v250, v[248:249], off offset:1024
	global_load_dword v251, v[248:249], off offset:1152
	v_mov_b32_e32 v145, 0xf149f2ca
	v_mov_b32_e32 v148, 0xf149f2ca
	s_waitcnt lgkmcnt(0)
	v_mfma_f32_16x16x32_bf16 v[26:29], v[26:29], v[2:5], v[36:39]
	s_nop 2
	s_waitcnt lgkmcnt(0)
	s_nop 3
	v_fmac_f32_e32 v240, 0x3e000000, v26
	v_cndmask_b32_e64 v148, v148, v240, s[28:29]
	s_nop 2
	s_waitcnt lgkmcnt(0)
	s_nop 0
	v_fmac_f32_e32 v241, 0x3e000000, v27
	v_cndmask_b32_e64 v145, v145, v241, s[30:31]
	v_mov_b32_e32 v149, 0xf149f2ca
	v_mov_b32_e32 v151, 0xf149f2ca
	s_nop 2
	s_waitcnt lgkmcnt(0)
	v_fmac_f32_e32 v242, 0x3e000000, v28
	v_cndmask_b32_e64 v151, v151, v242, s[34:35]
	s_nop 2
	s_waitcnt lgkmcnt(0)
	v_fmac_f32_e32 v243, 0x3e000000, v29
	v_cndmask_b32_e64 v149, v149, v243, s[36:37]
	ds_read_b128 v[26:29], v33 offset:18432
	ds_read_b128 v[36:39], v33 offset:18496
	v_mov_b32_e32 v152, 0xf149f2ca
	v_mov_b32_e32 v154, 0xf149f2ca
	s_waitcnt lgkmcnt(1)
	v_mfma_f32_16x16x32_bf16 v[26:29], v[26:29], v[6:9], 0
	s_waitcnt lgkmcnt(0)
	v_mfma_f32_16x16x32_bf16 v[26:29], v[36:39], v[2:5], v[26:29]
	s_nop 2
	s_waitcnt lgkmcnt(0)
	s_nop 3
	v_fmac_f32_e32 v244, 0x3e000000, v26
	v_cndmask_b32_e64 v154, v154, v244, s[38:39]
	s_nop 2
	s_waitcnt lgkmcnt(0)
	s_nop 0
	v_fmac_f32_e32 v245, 0x3e000000, v27
	v_cndmask_b32_e64 v152, v152, v245, s[44:45]
	v_mov_b32_e32 v153, 0xf149f2ca
	v_mov_b32_e32 v156, 0xf149f2ca
	s_nop 2
	s_waitcnt lgkmcnt(0)
	v_fmac_f32_e32 v246, 0x3e000000, v28
	v_cndmask_b32_e64 v156, v156, v246, s[46:47]
	s_nop 2
	s_waitcnt lgkmcnt(0)
	v_fmac_f32_e32 v247, 0x3e000000, v29
	v_cndmask_b32_e64 v153, v153, v247, s[48:49]
	v_max3_f32 v26, v91, s67, v90
	v_max3_f32 v26, v26, v93, v92
	v_max3_f32 v26, v26, v95, v94
	v_max3_f32 v26, v26, v99, v98
	v_max3_f32 v26, v26, v97, v96
	v_max3_f32 v26, v26, v101, v100
	v_max3_f32 v26, v26, v105, v103
	v_max3_f32 v26, v26, v109, v107
	v_max3_f32 v26, v26, v104, v102
	v_max3_f32 v26, v26, v108, v106
	v_max3_f32 v26, v26, v113, v110
	v_max3_f32 v26, v26, v116, v112
	v_max3_f32 v26, v26, v114, v111
	v_max3_f32 v26, v26, v117, v115
	v_max3_f32 v26, v26, v121, v118
	v_max3_f32 v26, v26, v124, v120
	v_max3_f32 v26, v26, v122, v119
	v_max3_f32 v26, v26, v125, v123
	v_max3_f32 v26, v26, v130, v127
	v_max3_f32 v26, v26, v134, v129
	v_max3_f32 v26, v26, v131, v128
	v_max3_f32 v26, v26, v135, v133
	v_max3_f32 v26, v26, v139, v136
	v_max3_f32 v26, v26, v142, v138
	v_max3_f32 v26, v26, v140, v137
	v_max3_f32 v26, v26, v143, v141
	v_mad_u32_u24 v88, v88, s64, v30
	v_max3_f32 v26, v26, v147, v144
	s_waitcnt vmcnt(7)
	ds_write_b128 v75, v[10:13]
	s_waitcnt vmcnt(6)
	ds_write_b128 v75, v[14:17] offset:9216
	s_waitcnt lgkmcnt(0)
	s_barrier
	ds_read_b128 v[10:13], v88
	ds_read_b128 v[14:17], v88 offset:64
	v_max3_f32 v26, v26, v150, v146
	v_max3_f32 v26, v26, v148, v145
	v_max3_f32 v26, v26, v151, v149
	v_max3_f32 v26, v26, v154, v152
	v_max3_f32 v35, v26, v156, v153
	v_or_b32_e32 v26, 0x80, v34
	v_mov_b64_e32 v[44:45], s[8:9]
	v_mad_i64_i32 v[26:27], s[28:29], v26, s57, v[44:45]
	v_lshl_add_u64 v[26:27], v[26:27], 0, v[70:71]
	v_lshl_add_u64 v[30:31], v[26:27], 0, s[2:3]
	s_waitcnt lgkmcnt(1)
	v_mfma_f32_16x16x32_bf16 v[10:13], v[10:13], v[6:9], 0
	v_lshl_add_u64 v[248:249], v[30:31], 0, s[100:101]
	global_load_dwordx4 v[26:29], v[30:31], off offset:1024
	s_nop 0
	global_load_dwordx4 v[30:33], v[30:31], off offset:1152
	global_load_dword v250, v[248:249], off offset:1024
	global_load_dword v251, v[248:249], off offset:1152
	ds_read_b128 v[36:39], v88 offset:2304
	v_lshl_add_u64 v[78:79], s[4:5], 0, v[70:71]
	s_waitcnt lgkmcnt(1)
	v_mfma_f32_16x16x32_bf16 v[62:65], v[14:17], v[2:5], v[10:13]
	s_ashr_i32 s17, s16, 31
	v_mov_b32_e32 v81, v71
	v_cmp_lt_i32_e32 vcc, v82, v83
	ds_read_b128 v[10:13], v88 offset:2368
	v_add3_u32 v155, v85, v76, v86
	s_nop 2
	v_mul_f32_e32 v14, 0x3e000000, v62
	v_mul_f32_e32 v15, 0x3e000000, v63
	v_max3_f32 v35, v35, v14, v15
	v_mul_f32_e32 v40, 0x3e000000, v64
	s_waitcnt lgkmcnt(1)
	v_mfma_f32_16x16x32_bf16 v[14:17], v[36:39], v[6:9], 0
	v_mul_f32_e32 v36, 0x3e000000, v65
	v_max3_f32 v35, v35, v40, v36
	ds_read_b128 v[36:39], v88 offset:4608
	s_waitcnt lgkmcnt(1)
	v_mfma_f32_16x16x32_bf16 v[66:69], v[10:13], v[2:5], v[14:17]
	ds_read_b128 v[10:13], v88 offset:4672
	s_ashr_i32 s19, s18, 31
	s_ashr_i32 s21, s20, 31
	s_ashr_i32 s23, s22, 31
	s_ashr_i32 s25, s24, 31
	s_nop 2
	v_mul_f32_e32 v14, 0x3e000000, v66
	v_mul_f32_e32 v15, 0x3e000000, v67
	v_max3_f32 v35, v35, v14, v15
	s_waitcnt lgkmcnt(1)
	v_mfma_f32_16x16x32_bf16 v[14:17], v[36:39], v[6:9], 0
	v_mul_f32_e32 v40, 0x3e000000, v68
	v_mul_f32_e32 v41, 0x3e000000, v69
	v_max3_f32 v35, v35, v40, v41
	s_waitcnt lgkmcnt(0)
	v_mfma_f32_16x16x32_bf16 v[58:61], v[10:13], v[2:5], v[14:17]
	ds_read_b128 v[36:39], v88 offset:6912
	ds_read_b128 v[40:43], v88 offset:6976
	s_waitcnt vmcnt(7)
	ds_write_b128 v75, v[18:21] offset:18432
	s_waitcnt vmcnt(6)
	ds_write_b128 v75, v[22:25] offset:27648
	s_waitcnt lgkmcnt(0)
	s_nop 0
	v_mul_f32_e32 v10, 0x3e000000, v58
	v_mul_f32_e32 v11, 0x3e000000, v59
	v_max3_f32 v14, v35, v10, v11
	v_mfma_f32_16x16x32_bf16 v[10:13], v[36:39], v[6:9], 0
	v_mul_f32_e32 v15, 0x3e000000, v60
	v_mul_f32_e32 v16, 0x3e000000, v61
	v_max3_f32 v14, v14, v15, v16
	v_mfma_f32_16x16x32_bf16 v[54:57], v[40:43], v[2:5], v[10:13]
	s_barrier
; #define LAS __attribute__((address_space(3)))
; template <bool LOCAL>
; __device__ __forceinline__ void na_unit(const bf16* P, const bf16* VT, bf16* YCAT, const LAS float* rpb_l, LAS bf16* buf, int b, int gr, int hp, int qblk, int tid) {
;     ...
;             } else {
;                 const int cc = c - NLOC;
; #pragma unroll
;                 for (int t4 = 0; t4 < 4; ++t4) {
;                     const LAS bf16* kp = cb + (16 * t4 + fr) * 72 + 8 * fq;
;                     f32x4 acc = {0.f, 0.f, 0.f, 0.f};
;                     acc = __builtin_amdgcn_mfma_f32_16x16x32_bf16(*(const LAS bf16x8*)(kp), qf[0], acc, 0, 0, 0);
;                     acc = __builtin_amdgcn_mfma_f32_16x16x32_bf16(*(const LAS bf16x8*)(kp + 32), qf[1], acc, 0, 0, 0);
; #pragma unroll
;                     for (int e = 0; e < 4; ++e) { acc[e] *= 0.125f; m = fmaxf(m, acc[e]); }
;                     sc[4 * (cc >= 0 ? cc : 0) + t4] = acc; }
;             }
;             if (sidx == NCH - 1) { m = fmaxf(m, __shfl_xor(m, 16)); m = fmaxf(m, __shfl_xor(m, 32)); }
	v_or_b32_e32 v18, 0xc0, v34
	v_mad_i64_i32 v[18:19], s[28:29], v18, s57, v[44:45]
	v_lshl_add_u64 v[18:19], v[18:19], 0, v[70:71]
	s_nop 3
	v_mul_f32_e32 v10, 0x3e000000, v54
	v_mul_f32_e32 v11, 0x3e000000, v55
	v_max3_f32 v14, v14, v10, v11
	ds_read_b128 v[10:13], v88 offset:18432
	v_mul_f32_e32 v15, 0x3e000000, v56
	v_mul_f32_e32 v16, 0x3e000000, v57
	v_max3_f32 v35, v14, v15, v16
	ds_read_b128 v[14:17], v88 offset:18496
	v_lshl_add_u64 v[22:23], v[18:19], 0, s[2:3]
	s_waitcnt lgkmcnt(1)
	v_mfma_f32_16x16x32_bf16 v[10:13], v[10:13], v[6:9], 0
	global_load_dwordx4 v[18:21], v[22:23], off offset:1024
	global_load_dwordx4 v[158:161], v[22:23], off offset:1152
	ds_read_b128 v[22:25], v88 offset:20736
	s_ashr_i32 s27, s26, 31
	s_waitcnt lgkmcnt(1)
	v_mfma_f32_16x16x32_bf16 v[46:49], v[14:17], v[2:5], v[10:13]
	s_nop 2
	ds_read_b128 v[10:13], v88 offset:20800
	s_nop 3
	v_mul_f32_e32 v14, 0x3e000000, v46
	v_mul_f32_e32 v15, 0x3e000000, v47
	v_max3_f32 v34, v35, v14, v15
	v_mul_f32_e32 v35, 0x3e000000, v48
	s_waitcnt lgkmcnt(1)
	v_mfma_f32_16x16x32_bf16 v[14:17], v[22:25], v[6:9], 0
	v_mul_f32_e32 v22, 0x3e000000, v49
	v_max3_f32 v34, v34, v35, v22
	ds_read_b128 v[22:25], v88 offset:23040
	s_waitcnt lgkmcnt(1)
	v_mfma_f32_16x16x32_bf16 v[50:53], v[10:13], v[2:5], v[14:17]
	ds_read_b128 v[10:13], v88 offset:23104
	s_nop 6
	v_mul_f32_e32 v14, 0x3e000000, v50
	v_mul_f32_e32 v15, 0x3e000000, v51
	v_max3_f32 v34, v34, v14, v15
	s_waitcnt lgkmcnt(1)
	v_mfma_f32_16x16x32_bf16 v[14:17], v[22:25], v[6:9], 0
	v_mul_f32_e32 v35, 0x3e000000, v52
	v_mul_f32_e32 v36, 0x3e000000, v53
	v_max3_f32 v38, v34, v35, v36
	s_waitcnt lgkmcnt(0)
	v_mfma_f32_16x16x32_bf16 v[42:45], v[10:13], v[2:5], v[14:17]
	ds_read_b128 v[22:25], v88 offset:25344
	ds_read_b128 v[34:37], v88 offset:25408
	s_waitcnt vmcnt(5)
	ds_write_b128 v75, v[26:29]
	s_waitcnt vmcnt(4)
	ds_write_b128 v75, v[30:33] offset:9216
	s_waitcnt lgkmcnt(0)
	s_nop 0
	v_mul_f32_e32 v10, 0x3e000000, v42
	v_mul_f32_e32 v11, 0x3e000000, v43
	v_max3_f32 v14, v38, v10, v11
	v_mfma_f32_16x16x32_bf16 v[10:13], v[22:25], v[6:9], 0
	v_mul_f32_e32 v15, 0x3e000000, v44
	v_mul_f32_e32 v16, 0x3e000000, v45
	v_max3_f32 v14, v14, v15, v16
	v_mfma_f32_16x16x32_bf16 v[38:41], v[34:37], v[2:5], v[10:13]
	s_barrier
	v_add3_u32 v26, v87, s1, 64
	v_mul_u32_u24_e32 v26, 0x9000, v26
	v_lshl_add_u64 v[22:23], s[16:17], 1, v[78:79]
	s_nop 3
	v_mul_f32_e32 v10, 0x3e000000, v38
	v_mul_f32_e32 v11, 0x3e000000, v39
	v_max3_f32 v10, v14, v10, v11
	v_mul_f32_e32 v11, 0x3e000000, v40
	v_mul_f32_e32 v12, 0x3e000000, v41
	v_max3_f32 v34, v10, v11, v12
	v_or_b32_e32 v10, s1, v87
	v_mul_u32_u24_e32 v14, 0x9000, v10
	ds_read_b128 v[10:13], v88
	v_lshlrev_b32_e32 v70, 1, v14
	ds_read_b128 v[14:17], v88 offset:64
	v_lshlrev_b32_e32 v80, 1, v26
	v_lshl_add_u64 v[24:25], v[22:23], 0, v[70:71]
	v_lshl_add_u64 v[22:23], v[22:23], 0, v[80:81]
	s_waitcnt lgkmcnt(1)
	v_mfma_f32_16x16x32_bf16 v[10:13], v[10:13], v[6:9], 0
	v_lshl_add_u64 v[248:249], v[24:25], 0, 0
	v_lshl_add_u64 v[238:239], v[22:23], 0, 0
	global_load_dwordx4 v[162:165], v[24:25], off
	global_load_dwordx4 v[166:169], v[22:23], off
	global_load_dword v250, v[248:249], off offset:128
	global_load_dword v251, v[238:239], off offset:128
	ds_read_b128 v[22:25], v88 offset:2304
	s_add_i32 s16, s15, s50
	s_waitcnt lgkmcnt(1)
	v_mfma_f32_16x16x32_bf16 v[30:33], v[14:17], v[2:5], v[10:13]
	s_ashr_i32 s17, s16, 31
	s_ashr_i32 s15, s14, 31
	s_ashr_i32 s1, s0, 31
	ds_read_b128 v[10:13], v88 offset:2368
	s_nop 3
	v_mul_f32_e32 v14, 0x3e000000, v30
	v_mul_f32_e32 v15, 0x3e000000, v31
	v_max3_f32 v26, v34, v14, v15
	v_mul_f32_e32 v27, 0x3e000000, v32
	s_waitcnt lgkmcnt(1)
	v_mfma_f32_16x16x32_bf16 v[14:17], v[22:25], v[6:9], 0
	v_mul_f32_e32 v22, 0x3e000000, v33
	v_max3_f32 v26, v26, v27, v22
	ds_read_b128 v[22:25], v88 offset:4608
	s_waitcnt lgkmcnt(1)
	v_mfma_f32_16x16x32_bf16 v[34:37], v[10:13], v[2:5], v[14:17]
	ds_read_b128 v[10:13], v88 offset:4672
	s_nop 6
	v_mul_f32_e32 v14, 0x3e000000, v34
	v_mul_f32_e32 v15, 0x3e000000, v35
	v_max3_f32 v26, v26, v14, v15
	s_waitcnt lgkmcnt(1)
	v_mfma_f32_16x16x32_bf16 v[14:17], v[22:25], v[6:9], 0
	v_mul_f32_e32 v27, 0x3e000000, v36
	v_mul_f32_e32 v28, 0x3e000000, v37
	v_max3_f32 v87, v26, v27, v28
	s_waitcnt lgkmcnt(0)
	v_mfma_f32_16x16x32_bf16 v[26:29], v[10:13], v[2:5], v[14:17]
	ds_read_b128 v[22:25], v88 offset:6912
	ds_read_b128 v[170:173], v88 offset:6976
	s_waitcnt vmcnt(5)
	ds_write_b128 v75, v[18:21] offset:18432
	s_waitcnt vmcnt(4)
	ds_write_b128 v75, v[158:161] offset:27648
	s_waitcnt lgkmcnt(0)
	s_nop 0
	v_mul_f32_e32 v10, 0x3e000000, v26
	v_mul_f32_e32 v11, 0x3e000000, v27
	v_max3_f32 v14, v87, v10, v11
	v_mfma_f32_16x16x32_bf16 v[10:13], v[22:25], v[6:9], 0
	v_mul_f32_e32 v15, 0x3e000000, v28
	v_mul_f32_e32 v16, 0x3e000000, v29
	v_max3_f32 v14, v14, v15, v16
	v_mfma_f32_16x16x32_bf16 v[22:25], v[170:173], v[2:5], v[10:13]
	s_barrier
; #define LAS __attribute__((address_space(3)))
; __device__ __forceinline__ unsigned cvt_pk_bf16(float lo, float hi) { const float __attribute__((ext_vector_type(2))) v = {lo, hi}; return __builtin_bit_cast(unsigned, __builtin_convertvector(v, bf16x2_t)); }
; template <bool LOCAL>
; __device__ __forceinline__ void na_unit(const bf16* P, const bf16* VT, bf16* YCAT, const LAS float* rpb_l, LAS bf16* buf, int b, int gr, int hp, int qblk, int tid) {
;     ...
;             if (sidx == NCH - 1) { m = fmaxf(m, __shfl_xor(m, 16)); m = fmaxf(m, __shfl_xor(m, 32)); }
;         } else {
;             const int c = sidx - NCH;
;             if (LOCAL && c < 8) {
;                 float p[8];
; #pragma unroll
;                 for (int e = 0; e < 4; ++e) { p[e] = __expf(sl[2 * (c < 8 ? c : 0)][e] - m); p[4 + e] = __expf(sl[2 * (c < 8 ? c : 0) + 1][e] - m); }
; #pragma unroll
;                 for (int e = 0; e < 8; ++e) lsum += p[e];
;                 const bf16x8 pf = __builtin_bit_cast(bf16x8, (v4u){pg8::cvt_pk_bf16(p[0], p[1]), pg8::cvt_pk_bf16(p[2], p[3]), pg8::cvt_pk_bf16(p[4], p[5]), pg8::cvt_pk_bf16(p[6], p[7])});
; #pragma unroll
;                 for (int dt = 0; dt < 4; ++dt) { const LAS bf16* vp = cb + (16 * dt + fr) * 72 + kc0 + 4 * fq;
;                     o[dt] = __builtin_amdgcn_mfma_f32_16x16x32_bf16(frag44(vp, vp + 16), pf, o[dt], 0, 0, 0); }
	v_lshl_add_u64 v[18:19], s[16:17], 1, v[78:79]
	v_lshl_add_u64 v[20:21], v[18:19], 0, v[70:71]
	v_lshl_add_u64 v[18:19], v[18:19], 0, v[80:81]
	s_nop 3
	v_mul_f32_e32 v10, 0x3e000000, v22
	v_mul_f32_e32 v11, 0x3e000000, v23
	v_max3_f32 v14, v14, v10, v11
	ds_read_b128 v[10:13], v88 offset:18432
	v_mul_f32_e32 v15, 0x3e000000, v24
	v_mul_f32_e32 v16, 0x3e000000, v25
	v_max3_f32 v87, v14, v15, v16
	ds_read_b128 v[14:17], v88 offset:18496
	s_waitcnt lgkmcnt(1)
	v_mfma_f32_16x16x32_bf16 v[10:13], v[10:13], v[6:9], 0
	v_lshl_add_u64 v[248:249], v[20:21], 0, 0
	v_lshl_add_u64 v[238:239], v[18:19], 0, 0
	global_load_dwordx4 v[158:161], v[20:21], off
	global_load_dwordx4 v[170:173], v[18:19], off
	global_load_dword v250, v[248:249], off offset:128
	global_load_dword v251, v[238:239], off offset:128
	ds_read_b128 v[18:21], v88 offset:20736
	ds_read_b128 v[174:177], v88 offset:23040
	s_waitcnt lgkmcnt(2)
	v_mfma_f32_16x16x32_bf16 v[14:17], v[14:17], v[2:5], v[10:13]
	s_nop 2
	ds_read_b128 v[10:13], v88 offset:20800
	s_waitcnt lgkmcnt(2)
	v_mfma_f32_16x16x32_bf16 v[18:21], v[18:21], v[6:9], 0
	s_nop 1
	v_mul_f32_e32 v126, 0x3e000000, v14
	v_mul_f32_e32 v132, 0x3e000000, v15
	v_max3_f32 v87, v87, v126, v132
	s_waitcnt lgkmcnt(0)
	v_mfma_f32_16x16x32_bf16 v[18:21], v[10:13], v[2:5], v[18:21]
	ds_read_b128 v[10:13], v88 offset:23104
	ds_read_b128 v[178:181], v88 offset:25344
	ds_read_b128 v[182:185], v88 offset:25408
	v_mul_f32_e32 v126, 0x3e000000, v16
	v_mfma_f32_16x16x32_bf16 v[174:177], v[174:177], v[6:9], 0
	v_mul_f32_e32 v132, 0x3e000000, v17
	v_max3_f32 v87, v87, v126, v132
	s_nop 0
	v_mul_f32_e32 v126, 0x3e000000, v18
	s_waitcnt lgkmcnt(1)
	v_mfma_f32_16x16x32_bf16 v[6:9], v[178:181], v[6:9], 0
	v_mul_f32_e32 v132, 0x3e000000, v19
	v_max3_f32 v87, v87, v126, v132
	v_mul_f32_e32 v126, 0x3e000000, v20
	v_mfma_f32_16x16x32_bf16 v[10:13], v[10:13], v[2:5], v[174:177]
	v_mul_f32_e32 v132, 0x3e000000, v21
	v_max3_f32 v87, v87, v126, v132
	s_waitcnt vmcnt(7)
	ds_write_b128 v75, v[162:165]
	s_waitcnt vmcnt(6)
	ds_write_b128 v75, v[166:169] offset:9216
	s_waitcnt lgkmcnt(2)
	v_mfma_f32_16x16x32_bf16 v[2:5], v[182:185], v[2:5], v[6:9]
	v_mul_f32_e32 v88, 0x3e000000, v10
	v_mul_f32_e32 v126, 0x3e000000, v11
	v_max3_f32 v87, v87, v88, v126
	v_mul_f32_e32 v88, 0x3e000000, v12
	v_mul_f32_e32 v126, 0x3e000000, v13
	v_max3_f32 v87, v87, v88, v126
	s_nop 1
	v_mul_f32_e32 v6, 0x3e000000, v2
	v_mul_f32_e32 v7, 0x3e000000, v3
	v_max3_f32 v6, v87, v6, v7
	v_mul_f32_e32 v7, 0x3e000000, v4
	v_mul_f32_e32 v8, 0x3e000000, v5
	v_max3_f32 v6, v6, v7, v8
	v_cndmask_b32_e32 v7, v1, v82, vcc
	v_lshlrev_b32_e32 v87, 2, v7
	ds_bpermute_b32 v7, v87, v6
	v_cmp_lt_i32_e32 vcc, v84, v83
	v_lshl_add_u32 v8, v89, 1, v155
	v_lshl_add_u64 v[182:183], s[14:15], 1, v[78:79]
	v_lshl_add_u64 v[184:185], v[182:183], 0, v[70:71]
	s_waitcnt lgkmcnt(0)
	v_max_f32_e32 v7, v7, v7
	v_max_f32_e32 v6, v6, v7
	v_cndmask_b32_e32 v7, v1, v84, vcc
	v_lshlrev_b32_e32 v88, 2, v7
	ds_bpermute_b32 v7, v88, v6
	v_lshl_add_u64 v[186:187], v[182:183], 0, v[80:81]
	s_waitcnt lgkmcnt(0)
	s_barrier
	v_max_f32_e32 v7, v7, v7
	v_max_f32_e32 v132, v6, v7
	v_sub_f32_e32 v6, v91, v132
	v_mul_f32_e32 v6, 0x3fb8aa3b, v6
	v_exp_f32_e32 v126, v6
	v_sub_f32_e32 v6, v95, v132
	v_mul_f32_e32 v6, 0x3fb8aa3b, v6
	v_exp_f32_e32 v91, v6
	v_sub_f32_e32 v6, v90, v132
	v_mul_f32_e32 v6, 0x3fb8aa3b, v6
	v_exp_f32_e32 v95, v6
	v_sub_f32_e32 v6, v94, v132
	v_mul_f32_e32 v6, 0x3fb8aa3b, v6
	v_exp_f32_e32 v90, v6
	v_sub_f32_e32 v6, v93, v132
	v_mul_f32_e32 v6, 0x3fb8aa3b, v6
	v_exp_f32_e32 v94, v6
	v_sub_f32_e32 v6, v99, v132
	v_mul_f32_e32 v6, 0x3fb8aa3b, v6
	v_exp_f32_e32 v93, v6
	v_sub_f32_e32 v6, v92, v132
	v_mul_f32_e32 v6, 0x3fb8aa3b, v6
	v_exp_f32_e32 v99, v6
	v_sub_f32_e32 v6, v98, v132
	v_mul_f32_e32 v6, 0x3fb8aa3b, v6
	v_exp_f32_e32 v92, v6
	v_add_u32_e32 v7, 0x800, v8
	v_add_u32_e32 v6, 0x1000, v8
	ds_read2_b64 v[162:165], v8 offset1:4
	ds_read2_b64 v[174:177], v7 offset0:32 offset1:36
	ds_read2_b64 v[178:181], v6 offset0:64 offset1:68
	v_lshl_add_u64 v[248:249], v[184:185], 0, 0
	v_lshl_add_u64 v[238:239], v[186:187], 0, 0
	global_load_dwordx4 v[182:185], v[184:185], off
	s_nop 0
	global_load_dwordx4 v[186:189], v[186:187], off
	global_load_dword v250, v[248:249], off offset:128
	global_load_dword v251, v[238:239], off offset:128
	v_sub_f32_e32 v9, v97, v132
	v_mul_f32_e32 v9, 0x3fb8aa3b, v9
	v_add_u32_e32 v157, 0x1800, v8
	v_exp_f32_e32 v85, v9
	v_sub_f32_e32 v9, v105, v132
	ds_read2_b64 v[190:193], v157 offset0:96 offset1:100
	v_mul_f32_e32 v9, 0x3fb8aa3b, v9
	v_exp_f32_e32 v76, v9
	v_sub_f32_e32 v9, v96, v132
	v_mul_f32_e32 v9, 0x3fb8aa3b, v9
	v_exp_f32_e32 v89, v9
	v_sub_f32_e32 v9, v103, v132
	v_mul_f32_e32 v9, 0x3fb8aa3b, v9
	v_exp_f32_e32 v86, v9
	v_sub_f32_e32 v9, v101, v132
	v_mul_f32_e32 v9, 0x3fb8aa3b, v9
	v_exp_f32_e32 v97, v9
	v_sub_f32_e32 v9, v109, v132
	v_cvt_pk_bf16_f32 v166, v126, v95
	v_cvt_pk_bf16_f32 v167, v94, v99
	v_cvt_pk_bf16_f32 v168, v91, v90
	v_cvt_pk_bf16_f32 v169, v93, v92
	s_waitcnt vmcnt(7)
	ds_write_b128 v75, v[158:161] offset:18432
	s_waitcnt vmcnt(6)
	ds_write_b128 v75, v[170:173] offset:27648
	v_mul_f32_e32 v9, 0x3fb8aa3b, v9
	v_add_u32_e32 v159, 0x4800, v8
	v_add_u32_e32 v158, 0x5000, v8
	s_waitcnt lgkmcnt(5)
	v_mfma_f32_16x16x32_bf16 v[162:165], v[162:165], v[166:169], 0
	s_waitcnt lgkmcnt(0)
	s_barrier
; #define LAS __attribute__((address_space(3)))
; __device__ __forceinline__ unsigned cvt_pk_bf16(float lo, float hi) { const float __attribute__((ext_vector_type(2))) v = {lo, hi}; return __builtin_bit_cast(unsigned, __builtin_convertvector(v, bf16x2_t)); }
; template <bool LOCAL>
; __device__ __forceinline__ void na_unit(const bf16* P, const bf16* VT, bf16* YCAT, const LAS float* rpb_l, LAS bf16* buf, int b, int gr, int hp, int qblk, int tid) {
;     ...
;             const int c = sidx - NCH;
;             if (LOCAL && c < 8) {
;                 float p[8];
; #pragma unroll
;                 for (int e = 0; e < 4; ++e) { p[e] = __expf(sl[2 * (c < 8 ? c : 0)][e] - m); p[4 + e] = __expf(sl[2 * (c < 8 ? c : 0) + 1][e] - m); }
; #pragma unroll
;                 for (int e = 0; e < 8; ++e) lsum += p[e];
;                 const bf16x8 pf = __builtin_bit_cast(bf16x8, (v4u){pg8::cvt_pk_bf16(p[0], p[1]), pg8::cvt_pk_bf16(p[2], p[3]), pg8::cvt_pk_bf16(p[4], p[5]), pg8::cvt_pk_bf16(p[6], p[7])});
; #pragma unroll
;                 for (int dt = 0; dt < 4; ++dt) { const LAS bf16* vp = cb + (16 * dt + fr) * 72 + kc0 + 4 * fq;
;                     o[dt] = __builtin_amdgcn_mfma_f32_16x16x32_bf16(frag44(vp, vp + 16), pf, o[dt], 0, 0, 0); }
	v_mfma_f32_16x16x32_bf16 v[174:177], v[174:177], v[166:169], 0
	v_exp_f32_e32 v96, v9
	v_sub_f32_e32 v9, v100, v132
	ds_read2_b64 v[170:173], v159 offset1:4
	v_mfma_f32_16x16x32_bf16 v[178:181], v[178:181], v[166:169], 0
	v_mul_f32_e32 v9, 0x3fb8aa3b, v9
	v_exp_f32_e32 v98, v9
	v_sub_f32_e32 v9, v107, v132
	v_mfma_f32_16x16x32_bf16 v[166:169], v[190:193], v[166:169], 0
	ds_read2_b64 v[190:193], v158 offset0:32 offset1:36
	v_mul_f32_e32 v9, 0x3fb8aa3b, v9
	v_exp_f32_e32 v100, v9
	v_lshl_add_u64 v[160:161], s[0:1], 1, v[78:79]
	v_cvt_pk_bf16_f32 v194, v85, v89
	v_cvt_pk_bf16_f32 v195, v97, v98
	v_cvt_pk_bf16_f32 v196, v76, v86
	v_cvt_pk_bf16_f32 v197, v96, v100
	v_lshl_add_u64 v[198:199], v[160:161], 0, v[70:71]
	v_lshl_add_u64 v[200:201], v[160:161], 0, v[80:81]
	v_add_u32_e32 v160, 0x5800, v8
	s_waitcnt lgkmcnt(1)
	v_mfma_f32_16x16x32_bf16 v[162:165], v[170:173], v[194:197], v[162:165]
	v_sub_f32_e32 v9, v104, v132
	v_mul_f32_e32 v9, 0x3fb8aa3b, v9
	v_add_u32_e32 v161, 0x6000, v8
	s_waitcnt lgkmcnt(0)
	v_mfma_f32_16x16x32_bf16 v[170:173], v[190:193], v[194:197], v[174:177]
	v_exp_f32_e32 v103, v9
	v_sub_f32_e32 v9, v113, v132
	v_mul_f32_e32 v9, 0x3fb8aa3b, v9
	ds_read2_b64 v[174:177], v160 offset0:64 offset1:68
	v_lshl_add_u64 v[248:249], v[198:199], 0, 0
	v_lshl_add_u64 v[238:239], v[200:201], 0, 0
	global_load_dwordx4 v[190:193], v[198:199], off
	s_nop 0
	global_load_dwordx4 v[198:201], v[200:201], off
	global_load_dword v250, v[248:249], off offset:128
	global_load_dword v251, v[238:239], off offset:128
	s_waitcnt lgkmcnt(0)
	v_mfma_f32_16x16x32_bf16 v[174:177], v[174:177], v[194:197], v[178:181]
	s_nop 2
	ds_read2_b64 v[178:181], v161 offset0:96 offset1:100
	v_exp_f32_e32 v101, v9
	v_sub_f32_e32 v9, v102, v132
	v_mul_f32_e32 v9, 0x3fb8aa3b, v9
	v_exp_f32_e32 v104, v9
	v_sub_f32_e32 v9, v110, v132
	v_mul_f32_e32 v9, 0x3fb8aa3b, v9
	v_exp_f32_e32 v102, v9
	v_sub_f32_e32 v9, v108, v132
	v_mul_f32_e32 v9, 0x3fb8aa3b, v9
	v_exp_f32_e32 v107, v9
	v_sub_f32_e32 v9, v116, v132
	v_mul_f32_e32 v9, 0x3fb8aa3b, v9
	s_waitcnt lgkmcnt(0)
	v_mfma_f32_16x16x32_bf16 v[166:169], v[178:181], v[194:197], v[166:169]
	s_waitcnt vmcnt(7)
	ds_write_b128 v75, v[182:185]
	s_waitcnt vmcnt(6)
	ds_write_b128 v75, v[186:189] offset:9216
	s_waitcnt lgkmcnt(0)
	s_barrier
	v_exp_f32_e32 v105, v9
	v_sub_f32_e32 v9, v106, v132
	ds_read2_b64 v[178:181], v8 offset1:4
	ds_read2_b64 v[182:185], v7 offset0:32 offset1:36
	v_mul_f32_e32 v9, 0x3fb8aa3b, v9
	v_exp_f32_e32 v106, v9
	v_sub_f32_e32 v9, v112, v132
	v_mul_f32_e32 v9, 0x3fb8aa3b, v9
	v_exp_f32_e32 v108, v9
	v_lshl_add_u64 v[194:195], s[18:19], 1, v[78:79]
	v_cvt_pk_bf16_f32 v186, v103, v104
	v_cvt_pk_bf16_f32 v187, v107, v106
	v_cvt_pk_bf16_f32 v188, v101, v102
	v_cvt_pk_bf16_f32 v189, v105, v108
	v_lshl_add_u64 v[112:113], v[194:195], 0, v[70:71]
	v_lshl_add_u64 v[194:195], v[194:195], 0, v[80:81]
	s_waitcnt lgkmcnt(1)
	v_mfma_f32_16x16x32_bf16 v[162:165], v[178:181], v[186:189], v[162:165]
	ds_read2_b64 v[178:181], v6 offset0:64 offset1:68
	v_sub_f32_e32 v9, v114, v132
	v_mul_f32_e32 v9, 0x3fb8aa3b, v9
	s_waitcnt lgkmcnt(1)
	v_mfma_f32_16x16x32_bf16 v[170:173], v[182:185], v[186:189], v[170:173]
	v_lshl_add_u64 v[248:249], v[112:113], 0, 0
	v_lshl_add_u64 v[238:239], v[194:195], 0, 0
	global_load_dwordx4 v[182:185], v[112:113], off
	s_nop 0
	global_load_dwordx4 v[194:197], v[194:195], off
	global_load_dword v250, v[248:249], off offset:128
	global_load_dword v251, v[238:239], off offset:128
	v_exp_f32_e32 v110, v9
	v_sub_f32_e32 v9, v121, v132
	s_waitcnt lgkmcnt(0)
	v_mfma_f32_16x16x32_bf16 v[174:177], v[178:181], v[186:189], v[174:177]
	ds_read2_b64 v[178:181], v157 offset0:96 offset1:100
	v_mul_f32_e32 v9, 0x3fb8aa3b, v9
	v_exp_f32_e32 v109, v9
	v_sub_f32_e32 v9, v111, v132
	v_mul_f32_e32 v9, 0x3fb8aa3b, v9
	v_exp_f32_e32 v112, v9
	v_sub_f32_e32 v9, v118, v132
	v_mul_f32_e32 v9, 0x3fb8aa3b, v9
	v_exp_f32_e32 v111, v9
	v_sub_f32_e32 v9, v117, v132
	v_mul_f32_e32 v9, 0x3fb8aa3b, v9
	v_exp_f32_e32 v114, v9
	v_sub_f32_e32 v9, v124, v132
	v_mul_f32_e32 v9, 0x3fb8aa3b, v9
	s_waitcnt lgkmcnt(0)
	v_mfma_f32_16x16x32_bf16 v[166:169], v[178:181], v[186:189], v[166:169]
	s_waitcnt vmcnt(7)
	ds_write_b128 v75, v[190:193] offset:18432
	s_waitcnt vmcnt(6)
	ds_write_b128 v75, v[198:201] offset:27648
	s_waitcnt lgkmcnt(0)
	s_barrier
	v_exp_f32_e32 v113, v9
	v_sub_f32_e32 v9, v115, v132
	ds_read2_b64 v[178:181], v159 offset1:4
	v_mul_f32_e32 v9, 0x3fb8aa3b, v9
	v_exp_f32_e32 v115, v9
	v_sub_f32_e32 v9, v120, v132
	v_mul_f32_e32 v9, 0x3fb8aa3b, v9
	v_exp_f32_e32 v116, v9
	v_lshl_add_u64 v[198:199], s[20:21], 1, v[78:79]
	v_lshl_add_u64 v[200:201], v[198:199], 0, v[70:71]
	ds_read2_b64 v[186:189], v158 offset0:32 offset1:36
	v_cvt_pk_bf16_f32 v190, v110, v112
	v_cvt_pk_bf16_f32 v191, v114, v115
	v_cvt_pk_bf16_f32 v192, v109, v111
	v_cvt_pk_bf16_f32 v193, v113, v116
	v_lshl_add_u64 v[120:121], v[198:199], 0, v[80:81]
	v_sub_f32_e32 v9, v122, v132
	s_waitcnt lgkmcnt(1)
	v_mfma_f32_16x16x32_bf16 v[162:165], v[178:181], v[190:193], v[162:165]
	v_lshl_add_u64 v[248:249], v[200:201], 0, 0
	v_lshl_add_u64 v[238:239], v[120:121], 0, 0
	global_load_dwordx4 v[178:181], v[200:201], off
	s_nop 0
	global_load_dwordx4 v[198:201], v[120:121], off
	global_load_dword v250, v[248:249], off offset:128
	global_load_dword v251, v[238:239], off offset:128
	v_mul_f32_e32 v9, 0x3fb8aa3b, v9
	v_exp_f32_e32 v118, v9
	s_waitcnt lgkmcnt(0)
	v_mfma_f32_16x16x32_bf16 v[170:173], v[186:189], v[190:193], v[170:173]
	ds_read2_b64 v[186:189], v160 offset0:64 offset1:68
	v_sub_f32_e32 v9, v130, v132
	v_mul_f32_e32 v9, 0x3fb8aa3b, v9
	s_waitcnt lgkmcnt(0)
	v_mfma_f32_16x16x32_bf16 v[174:177], v[186:189], v[190:193], v[174:177]
	ds_read2_b64 v[186:189], v161 offset0:96 offset1:100
	v_exp_f32_e32 v117, v9
	v_sub_f32_e32 v9, v119, v132
	v_mul_f32_e32 v9, 0x3fb8aa3b, v9
	v_exp_f32_e32 v120, v9
	v_sub_f32_e32 v9, v127, v132
	v_mul_f32_e32 v9, 0x3fb8aa3b, v9
	v_exp_f32_e32 v119, v9
	v_sub_f32_e32 v9, v125, v132
	v_mul_f32_e32 v9, 0x3fb8aa3b, v9
	v_exp_f32_e32 v122, v9
	v_sub_f32_e32 v9, v134, v132
	v_mul_f32_e32 v9, 0x3fb8aa3b, v9
	s_waitcnt lgkmcnt(0)
	v_mfma_f32_16x16x32_bf16 v[166:169], v[186:189], v[190:193], v[166:169]
	s_waitcnt vmcnt(7)
	ds_write_b128 v75, v[182:185]
	s_waitcnt vmcnt(6)
	ds_write_b128 v75, v[194:197] offset:9216
	s_waitcnt lgkmcnt(0)
	s_barrier
; #define LAS __attribute__((address_space(3)))
; __device__ __forceinline__ unsigned cvt_pk_bf16(float lo, float hi) { const float __attribute__((ext_vector_type(2))) v = {lo, hi}; return __builtin_bit_cast(unsigned, __builtin_convertvector(v, bf16x2_t)); }
; template <bool LOCAL>
; __device__ __forceinline__ void na_unit(const bf16* P, const bf16* VT, bf16* YCAT, const LAS float* rpb_l, LAS bf16* buf, int b, int gr, int hp, int qblk, int tid) {
;     ...
;             const int c = sidx - NCH;
;             if (LOCAL && c < 8) {
;                 float p[8];
; #pragma unroll
;                 for (int e = 0; e < 4; ++e) { p[e] = __expf(sl[2 * (c < 8 ? c : 0)][e] - m); p[4 + e] = __expf(sl[2 * (c < 8 ? c : 0) + 1][e] - m); }
; #pragma unroll
;                 for (int e = 0; e < 8; ++e) lsum += p[e];
;                 const bf16x8 pf = __builtin_bit_cast(bf16x8, (v4u){pg8::cvt_pk_bf16(p[0], p[1]), pg8::cvt_pk_bf16(p[2], p[3]), pg8::cvt_pk_bf16(p[4], p[5]), pg8::cvt_pk_bf16(p[6], p[7])});
; #pragma unroll
;                 for (int dt = 0; dt < 4; ++dt) { const LAS bf16* vp = cb + (16 * dt + fr) * 72 + kc0 + 4 * fq;
;                     o[dt] = __builtin_amdgcn_mfma_f32_16x16x32_bf16(frag44(vp, vp + 16), pf, o[dt], 0, 0, 0); }
	v_exp_f32_e32 v121, v9
	v_sub_f32_e32 v9, v123, v132
	ds_read2_b64 v[182:185], v8 offset1:4
	ds_read2_b64 v[186:189], v7 offset0:32 offset1:36
	v_mul_f32_e32 v9, 0x3fb8aa3b, v9
	v_exp_f32_e32 v123, v9
	v_sub_f32_e32 v9, v129, v132
	v_mul_f32_e32 v9, 0x3fb8aa3b, v9
	v_exp_f32_e32 v124, v9
	v_lshl_add_u64 v[194:195], s[22:23], 1, v[78:79]
	v_cvt_pk_bf16_f32 v190, v118, v120
	v_cvt_pk_bf16_f32 v191, v122, v123
	v_cvt_pk_bf16_f32 v192, v117, v119
	v_cvt_pk_bf16_f32 v193, v121, v124
	v_lshl_add_u64 v[196:197], v[194:195], 0, v[70:71]
	v_lshl_add_u64 v[194:195], v[194:195], 0, v[80:81]
	s_waitcnt lgkmcnt(1)
	v_mfma_f32_16x16x32_bf16 v[162:165], v[182:185], v[190:193], v[162:165]
	ds_read2_b64 v[182:185], v6 offset0:64 offset1:68
	v_sub_f32_e32 v9, v131, v132
	v_mul_f32_e32 v9, 0x3fb8aa3b, v9
	s_waitcnt lgkmcnt(1)
	v_mfma_f32_16x16x32_bf16 v[170:173], v[186:189], v[190:193], v[170:173]
	v_lshl_add_u64 v[248:249], v[196:197], 0, 0
	v_lshl_add_u64 v[238:239], v[194:195], 0, 0
	global_load_dwordx4 v[186:189], v[196:197], off
	s_nop 0
	global_load_dwordx4 v[194:197], v[194:195], off
	global_load_dword v250, v[248:249], off offset:128
	global_load_dword v251, v[238:239], off offset:128
	v_exp_f32_e32 v127, v9
	v_sub_f32_e32 v9, v139, v132
	v_mul_f32_e32 v9, 0x3fb8aa3b, v9
	v_exp_f32_e32 v125, v9
	v_sub_f32_e32 v9, v128, v132
	v_mul_f32_e32 v9, 0x3fb8aa3b, v9
	v_exp_f32_e32 v129, v9
	v_sub_f32_e32 v9, v136, v132
	v_mul_f32_e32 v9, 0x3fb8aa3b, v9
	v_exp_f32_e32 v128, v9
	v_sub_f32_e32 v9, v135, v132
	v_mul_f32_e32 v9, 0x3fb8aa3b, v9
	v_exp_f32_e32 v131, v9
	v_sub_f32_e32 v9, v142, v132
	s_waitcnt lgkmcnt(0)
	v_mfma_f32_16x16x32_bf16 v[174:177], v[182:185], v[190:193], v[174:177]
	ds_read2_b64 v[182:185], v157 offset0:96 offset1:100
	v_mul_f32_e32 v9, 0x3fb8aa3b, v9
	s_waitcnt vmcnt(7)
	ds_write_b128 v75, v[178:181] offset:18432
	s_waitcnt vmcnt(6)
	ds_write_b128 v75, v[198:201] offset:27648
	s_waitcnt lgkmcnt(0)
	s_barrier
	v_exp_f32_e32 v130, v9
	v_sub_f32_e32 v9, v133, v132
	ds_read2_b64 v[178:181], v159 offset1:4
	v_mul_f32_e32 v9, 0x3fb8aa3b, v9
	v_exp_f32_e32 v133, v9
	v_sub_f32_e32 v9, v138, v132
	v_mul_f32_e32 v9, 0x3fb8aa3b, v9
	v_exp_f32_e32 v134, v9
	v_lshl_add_u64 v[198:199], s[24:25], 1, v[78:79]
	v_mfma_f32_16x16x32_bf16 v[166:169], v[182:185], v[190:193], v[166:169]
	v_lshl_add_u64 v[200:201], v[198:199], 0, v[70:71]
	ds_read2_b64 v[182:185], v158 offset0:32 offset1:36
	v_cvt_pk_bf16_f32 v190, v127, v129
	v_cvt_pk_bf16_f32 v191, v131, v133
	v_cvt_pk_bf16_f32 v192, v125, v128
	v_cvt_pk_bf16_f32 v193, v130, v134
	v_lshl_add_u64 v[138:139], v[198:199], 0, v[80:81]
	v_sub_f32_e32 v9, v140, v132
	s_waitcnt lgkmcnt(1)
	v_mfma_f32_16x16x32_bf16 v[162:165], v[178:181], v[190:193], v[162:165]
	global_load_dwordx4 v[178:181], v[200:201], off
	s_nop 0
	global_load_dwordx4 v[198:201], v[138:139], off
	v_mul_f32_e32 v9, 0x3fb8aa3b, v9
	v_exp_f32_e32 v136, v9
	s_waitcnt lgkmcnt(0)
	v_mfma_f32_16x16x32_bf16 v[170:173], v[182:185], v[190:193], v[170:173]
	ds_read2_b64 v[182:185], v160 offset0:64 offset1:68
	v_sub_f32_e32 v9, v147, v132
	v_mul_f32_e32 v9, 0x3fb8aa3b, v9
	s_waitcnt lgkmcnt(0)
	v_mfma_f32_16x16x32_bf16 v[174:177], v[182:185], v[190:193], v[174:177]
	ds_read2_b64 v[182:185], v161 offset0:96 offset1:100
	v_exp_f32_e32 v135, v9
	v_sub_f32_e32 v9, v137, v132
	v_mul_f32_e32 v9, 0x3fb8aa3b, v9
	v_exp_f32_e32 v138, v9
	v_sub_f32_e32 v9, v144, v132
	v_mul_f32_e32 v9, 0x3fb8aa3b, v9
	v_exp_f32_e32 v137, v9
	v_sub_f32_e32 v9, v143, v132
	v_mul_f32_e32 v9, 0x3fb8aa3b, v9
	s_waitcnt lgkmcnt(0)
	v_mfma_f32_16x16x32_bf16 v[166:169], v[182:185], v[190:193], v[166:169]
	s_waitcnt vmcnt(5)
	ds_write_b128 v75, v[186:189]
	s_waitcnt vmcnt(4)
	ds_write_b128 v75, v[194:197] offset:9216
	s_waitcnt lgkmcnt(0)
	s_barrier
	v_exp_f32_e32 v140, v9
	v_sub_f32_e32 v9, v150, v132
	ds_read2_b64 v[182:185], v8 offset1:4
	v_mul_f32_e32 v9, 0x3fb8aa3b, v9
	ds_read2_b64 v[190:193], v7 offset0:32 offset1:36
	v_exp_f32_e32 v139, v9
	v_sub_f32_e32 v9, v141, v132
	v_sub_f32_e32 v8, v146, v132
	v_mul_f32_e32 v9, 0x3fb8aa3b, v9
	v_mul_f32_e32 v8, 0x3fb8aa3b, v8
	v_exp_f32_e32 v141, v9
	v_exp_f32_e32 v142, v8
	v_cvt_pk_bf16_f32 v186, v136, v138
	v_cvt_pk_bf16_f32 v188, v135, v137
	v_cvt_pk_bf16_f32 v187, v140, v141
	v_cvt_pk_bf16_f32 v189, v139, v142
	v_lshl_add_u64 v[8:9], s[26:27], 1, v[78:79]
	v_sub_f32_e32 v144, v149, v132
	s_waitcnt lgkmcnt(1)
	v_mfma_f32_16x16x32_bf16 v[162:165], v[182:185], v[186:189], v[162:165]
	ds_read2_b64 v[182:185], v6 offset0:64 offset1:68
	v_lshl_add_u64 v[6:7], v[8:9], 0, v[70:71]
	v_lshl_add_u64 v[8:9], v[8:9], 0, v[80:81]
	s_waitcnt lgkmcnt(1)
	v_mfma_f32_16x16x32_bf16 v[170:173], v[190:193], v[186:189], v[170:173]
	v_lshl_add_u64 v[248:249], v[6:7], 0, 0
	v_lshl_add_u64 v[238:239], v[8:9], 0, 0
	global_load_dwordx4 v[190:193], v[6:7], off
	global_load_dwordx4 v[194:197], v[8:9], off
	global_load_dword v250, v[248:249], off offset:128
	global_load_dword v251, v[238:239], off offset:128
	ds_read2_b64 v[78:81], v157 offset0:96 offset1:100
	s_waitcnt vmcnt(5)
	ds_write_b128 v75, v[178:181] offset:18432
	s_waitcnt vmcnt(4)
	ds_write_b128 v75, v[198:201] offset:27648
	s_waitcnt lgkmcnt(2)
	v_mfma_f32_16x16x32_bf16 v[166:169], v[78:81], v[186:189], v[166:169]
	s_waitcnt lgkmcnt(0)
	s_barrier
; #define LAS __attribute__((address_space(3)))
; __device__ __forceinline__ unsigned cvt_pk_bf16(float lo, float hi) { const float __attribute__((ext_vector_type(2))) v = {lo, hi}; return __builtin_bit_cast(unsigned, __builtin_convertvector(v, bf16x2_t)); }
; template <bool LOCAL>
; __device__ __forceinline__ void na_unit(const bf16* P, const bf16* VT, bf16* YCAT, const LAS float* rpb_l, LAS bf16* buf, int b, int gr, int hp, int qblk, int tid) {
;     ...
;             const int c = sidx - NCH;
;             if (LOCAL && c < 8) {
;                 float p[8];
; #pragma unroll
;                 for (int e = 0; e < 4; ++e) { p[e] = __expf(sl[2 * (c < 8 ? c : 0)][e] - m); p[4 + e] = __expf(sl[2 * (c < 8 ? c : 0) + 1][e] - m); }
; #pragma unroll
;                 for (int e = 0; e < 8; ++e) lsum += p[e];
;                 const bf16x8 pf = __builtin_bit_cast(bf16x8, (v4u){pg8::cvt_pk_bf16(p[0], p[1]), pg8::cvt_pk_bf16(p[2], p[3]), pg8::cvt_pk_bf16(p[4], p[5]), pg8::cvt_pk_bf16(p[6], p[7])});
; #pragma unroll
;                 for (int dt = 0; dt < 4; ++dt) { const LAS bf16* vp = cb + (16 * dt + fr) * 72 + kc0 + 4 * fq;
;                     o[dt] = __builtin_amdgcn_mfma_f32_16x16x32_bf16(frag44(vp, vp + 16), pf, o[dt], 0, 0, 0); }
;             } else {
;                 const int cc = c - NLOC;
; #pragma unroll
;                 for (int p2 = 0; p2 < 2; ++p2) {
;                     float p[8];
; #pragma unroll
;                     for (int e = 0; e < 4; ++e) { p[e] = __expf(sc[4 * (cc >= 0 ? cc : 0) + 2 * p2][e] - m); p[4 + e] = __expf(sc[4 * (cc >= 0 ? cc : 0) + 2 * p2 + 1][e] - m); }
; #pragma unroll
;                     for (int e = 0; e < 8; ++e) lsum += p[e];
;                     const bf16x8 pf = __builtin_bit_cast(bf16x8, (v4u){pg8::cvt_pk_bf16(p[0], p[1]), pg8::cvt_pk_bf16(p[2], p[3]), pg8::cvt_pk_bf16(p[4], p[5]), pg8::cvt_pk_bf16(p[6], p[7])});
; #pragma unroll
;                     for (int dt = 0; dt < 4; ++dt) { const LAS bf16* vp = cb + (16 * dt + fr) * 72 + 32 * p2 + 4 * fq;
;                         o[dt] = __builtin_amdgcn_mfma_f32_16x16x32_bf16(frag44(vp, vp + 16), pf, o[dt], 0, 0, 0); }
;                 }
	v_sub_f32_e32 v70, v148, v132
	v_sub_f32_e32 v79, v145, v132
	v_sub_f32_e32 v81, v151, v132
	ds_read2_b64 v[146:149], v159 offset1:4
	v_mul_f32_e32 v70, 0x3fb8aa3b, v70
	v_mul_f32_e32 v79, 0x3fb8aa3b, v79
	v_mul_f32_e32 v81, 0x3fb8aa3b, v81
	v_mul_f32_e32 v144, 0x3fb8aa3b, v144
	v_exp_f32_e32 v78, v70
	v_sub_f32_e32 v70, v154, v132
	v_exp_f32_e32 v80, v79
	v_sub_f32_e32 v79, v152, v132
	v_exp_f32_e32 v143, v81
	v_sub_f32_e32 v81, v156, v132
	v_exp_f32_e32 v145, v144
	v_sub_f32_e32 v144, v153, v132
	v_mul_f32_e32 v70, 0x3fb8aa3b, v70
	v_mul_f32_e32 v79, 0x3fb8aa3b, v79
	v_mul_f32_e32 v81, 0x3fb8aa3b, v81
	v_mul_f32_e32 v144, 0x3fb8aa3b, v144
	v_exp_f32_e32 v70, v70
	v_exp_f32_e32 v79, v79
	v_exp_f32_e32 v81, v81
	v_exp_f32_e32 v144, v144
	v_cvt_pk_bf16_f32 v150, v78, v80
	v_cvt_pk_bf16_f32 v151, v143, v145
	v_cvt_pk_bf16_f32 v152, v70, v79
	v_cvt_pk_bf16_f32 v153, v81, v144
	v_mfma_f32_16x16x32_bf16 v[174:177], v[182:185], v[186:189], v[174:177]
	v_fma_f32 v62, v62, s66, -v132
	v_fma_f32 v63, v63, s66, -v132
	v_fma_f32 v64, v64, s66, -v132
	s_waitcnt lgkmcnt(0)
	v_mfma_f32_16x16x32_bf16 v[162:165], v[146:149], v[150:153], v[162:165]
	ds_read2_b64 v[146:149], v158 offset0:32 offset1:36
	v_fma_f32 v65, v65, s66, -v132
	v_mul_f32_e32 v62, 0x3fb8aa3b, v62
	s_waitcnt lgkmcnt(0)
	v_mfma_f32_16x16x32_bf16 v[156:159], v[146:149], v[150:153], v[170:173]
	ds_read2_b64 v[146:149], v160 offset0:64 offset1:68
	v_mul_f32_e32 v63, 0x3fb8aa3b, v63
	v_mul_f32_e32 v64, 0x3fb8aa3b, v64
	s_waitcnt lgkmcnt(0)
	v_mfma_f32_16x16x32_bf16 v[170:173], v[146:149], v[150:153], v[174:177]
	ds_read2_b64 v[146:149], v161 offset0:96 offset1:100
	s_nop 1
	v_lshl_add_u64 v[248:249], v[6:7], 0, 0
	v_lshl_add_u64 v[238:239], v[8:9], 0, 0
	global_load_dwordx4 v[174:177], v[6:7], off offset:128
	global_load_dwordx4 v[178:181], v[8:9], off offset:128
	global_load_dword v250, v[248:249], off offset:256
	global_load_dword v251, v[238:239], off offset:256
	s_waitcnt vmcnt(7)
	ds_write_b128 v75, v[190:193]
	s_waitcnt vmcnt(6)
	ds_write_b128 v75, v[194:197] offset:9216
	s_waitcnt lgkmcnt(2)
	v_mfma_f32_16x16x32_bf16 v[148:151], v[146:149], v[150:153], v[166:169]
	s_waitcnt lgkmcnt(0)
	s_barrier
	s_nop 0
	ds_read2_b64 v[166:169], v155 offset1:4
	v_mul_f32_e32 v65, 0x3fb8aa3b, v65
	v_exp_f32_e32 v146, v62
	v_fma_f32 v62, v66, s66, -v132
	v_exp_f32_e32 v66, v63
	v_fma_f32 v63, v67, s66, -v132
	v_exp_f32_e32 v67, v64
	v_fma_f32 v64, v68, s66, -v132
	v_exp_f32_e32 v68, v65
	v_fma_f32 v65, v69, s66, -v132
	v_mul_f32_e32 v62, 0x3fb8aa3b, v62
	v_mul_f32_e32 v63, 0x3fb8aa3b, v63
	v_mul_f32_e32 v64, 0x3fb8aa3b, v64
	v_mul_f32_e32 v65, 0x3fb8aa3b, v65
	v_exp_f32_e32 v62, v62
	v_exp_f32_e32 v63, v63
	v_exp_f32_e32 v64, v64
	v_exp_f32_e32 v65, v65
	v_cvt_pk_bf16_f32 v182, v146, v66
	v_cvt_pk_bf16_f32 v183, v67, v68
	v_cvt_pk_bf16_f32 v184, v62, v63
	v_cvt_pk_bf16_f32 v185, v64, v65
	v_add_u32_e32 v147, 0x800, v155
	v_add_u32_e32 v152, 0x1000, v155
	s_waitcnt lgkmcnt(0)
	v_mfma_f32_16x16x32_bf16 v[160:163], v[166:169], v[182:185], v[162:165]
	v_add_u32_e32 v153, 0x1800, v155
	v_fma_f32 v58, v58, s66, -v132
	v_fma_f32 v54, v54, s66, -v132
	ds_read2_b64 v[164:167], v147 offset0:32 offset1:36
	s_waitcnt lgkmcnt(0)
	v_mfma_f32_16x16x32_bf16 v[156:159], v[164:167], v[182:185], v[156:159]
	ds_read2_b64 v[164:167], v152 offset0:64 offset1:68
	v_fma_f32 v59, v59, s66, -v132
	v_fma_f32 v55, v55, s66, -v132
	s_waitcnt lgkmcnt(0)
	v_mfma_f32_16x16x32_bf16 v[164:167], v[164:167], v[182:185], v[170:173]
	s_nop 2
	ds_read2_b64 v[168:171], v153 offset0:96 offset1:100
	v_fma_f32 v60, v60, s66, -v132
	v_fma_f32 v56, v56, s66, -v132
	s_waitcnt lgkmcnt(0)
	v_mfma_f32_16x16x32_bf16 v[148:151], v[168:171], v[182:185], v[148:151]
	ds_read2_b64 v[168:171], v155 offset0:8 offset1:12
	v_fma_f32 v61, v61, s66, -v132
	v_fma_f32 v57, v57, s66, -v132
	v_mul_f32_e32 v58, 0x3fb8aa3b, v58
	v_mul_f32_e32 v54, 0x3fb8aa3b, v54
	v_mul_f32_e32 v59, 0x3fb8aa3b, v59
	v_mul_f32_e32 v55, 0x3fb8aa3b, v55
	v_mul_f32_e32 v60, 0x3fb8aa3b, v60
	v_mul_f32_e32 v56, 0x3fb8aa3b, v56
	v_mul_f32_e32 v61, 0x3fb8aa3b, v61
	v_mul_f32_e32 v57, 0x3fb8aa3b, v57
	v_exp_f32_e32 v58, v58
	v_exp_f32_e32 v54, v54
	v_exp_f32_e32 v59, v59
	v_exp_f32_e32 v55, v55
	v_exp_f32_e32 v60, v60
	v_exp_f32_e32 v56, v56
	v_exp_f32_e32 v61, v61
	v_exp_f32_e32 v57, v57
	v_cvt_pk_bf16_f32 v182, v58, v59
	v_cvt_pk_bf16_f32 v184, v54, v55
	v_cvt_pk_bf16_f32 v183, v60, v61
	v_cvt_pk_bf16_f32 v185, v56, v57
	v_fma_f32 v46, v46, s66, -v132
	v_fma_f32 v47, v47, s66, -v132
	s_waitcnt lgkmcnt(0)
	v_mfma_f32_16x16x32_bf16 v[160:163], v[168:171], v[182:185], v[160:163]
	ds_read2_b64 v[168:171], v147 offset0:40 offset1:44
	v_fma_f32 v48, v48, s66, -v132
	v_mul_f32_e32 v46, 0x3fb8aa3b, v46
	s_waitcnt lgkmcnt(0)
	v_mfma_f32_16x16x32_bf16 v[156:159], v[168:171], v[182:185], v[156:159]
	ds_read2_b64 v[168:171], v152 offset0:72 offset1:76
	v_mul_f32_e32 v47, 0x3fb8aa3b, v47
	v_mul_f32_e32 v48, 0x3fb8aa3b, v48
	s_waitcnt lgkmcnt(0)
	v_mfma_f32_16x16x32_bf16 v[164:167], v[168:171], v[182:185], v[164:167]
	ds_read2_b64 v[168:171], v153 offset0:104 offset1:108
	v_exp_f32_e32 v69, v46
	v_fma_f32 v46, v50, s66, -v132
	v_exp_f32_e32 v50, v47
	v_fma_f32 v47, v51, s66, -v132
	v_exp_f32_e32 v51, v48
	v_fma_f32 v48, v52, s66, -v132
	v_add_u32_e32 v52, 0x4800, v155
	v_lshl_add_u64 v[248:249], v[6:7], 0, 0
	v_lshl_add_u64 v[238:239], v[8:9], 0, 0
	global_load_dwordx4 v[186:189], v[6:7], off offset:256
	global_load_dwordx4 v[190:193], v[8:9], off offset:256
	global_load_dword v250, v[248:249], off offset:384
	global_load_dword v251, v[238:239], off offset:384
	s_waitcnt lgkmcnt(0)
	v_mfma_f32_16x16x32_bf16 v[148:151], v[168:171], v[182:185], v[148:151]
	s_waitcnt vmcnt(7)
	ds_write_b128 v75, v[174:177] offset:18432
	s_waitcnt vmcnt(6)
	ds_write_b128 v75, v[178:181] offset:27648
	s_waitcnt lgkmcnt(0)
	s_barrier
; #define LAS __attribute__((address_space(3)))
; __device__ __forceinline__ unsigned cvt_pk_bf16(float lo, float hi) { const float __attribute__((ext_vector_type(2))) v = {lo, hi}; return __builtin_bit_cast(unsigned, __builtin_convertvector(v, bf16x2_t)); }
; template <bool LOCAL>
; __device__ __forceinline__ void na_unit(const bf16* P, const bf16* VT, bf16* YCAT, const LAS float* rpb_l, LAS bf16* buf, int b, int gr, int hp, int qblk, int tid) {
;     ...
;                 const int cc = c - NLOC;
; #pragma unroll
;                 for (int p2 = 0; p2 < 2; ++p2) {
;                     float p[8];
; #pragma unroll
;                     for (int e = 0; e < 4; ++e) { p[e] = __expf(sc[4 * (cc >= 0 ? cc : 0) + 2 * p2][e] - m); p[4 + e] = __expf(sc[4 * (cc >= 0 ? cc : 0) + 2 * p2 + 1][e] - m); }
; #pragma unroll
;                     for (int e = 0; e < 8; ++e) lsum += p[e];
;                     const bf16x8 pf = __builtin_bit_cast(bf16x8, (v4u){pg8::cvt_pk_bf16(p[0], p[1]), pg8::cvt_pk_bf16(p[2], p[3]), pg8::cvt_pk_bf16(p[4], p[5]), pg8::cvt_pk_bf16(p[6], p[7])});
; #pragma unroll
;                     for (int dt = 0; dt < 4; ++dt) { const LAS bf16* vp = cb + (16 * dt + fr) * 72 + 32 * p2 + 4 * fq;
;                         o[dt] = __builtin_amdgcn_mfma_f32_16x16x32_bf16(frag44(vp, vp + 16), pf, o[dt], 0, 0, 0); }
;                 }
	v_fma_f32 v49, v49, s66, -v132
	ds_read2_b64 v[168:171], v52 offset1:4
	v_mul_f32_e32 v49, 0x3fb8aa3b, v49
	v_exp_f32_e32 v154, v49
	v_fma_f32 v49, v53, s66, -v132
	v_mul_f32_e32 v46, 0x3fb8aa3b, v46
	v_mul_f32_e32 v47, 0x3fb8aa3b, v47
	v_mul_f32_e32 v48, 0x3fb8aa3b, v48
	v_mul_f32_e32 v49, 0x3fb8aa3b, v49
	v_exp_f32_e32 v46, v46
	v_exp_f32_e32 v47, v47
	v_exp_f32_e32 v48, v48
	v_exp_f32_e32 v53, v49
	v_cvt_pk_bf16_f32 v172, v69, v50
	v_cvt_pk_bf16_f32 v173, v51, v154
	v_cvt_pk_bf16_f32 v174, v46, v47
	v_cvt_pk_bf16_f32 v175, v48, v53
	v_add_u32_e32 v176, 0x5000, v155
	v_add_u32_e32 v177, 0x5800, v155
	s_waitcnt lgkmcnt(0)
	v_mfma_f32_16x16x32_bf16 v[160:163], v[168:171], v[172:175], v[160:163]
	ds_read2_b64 v[168:171], v176 offset0:32 offset1:36
	v_add_u32_e32 v49, 0x6000, v155
	v_fma_f32 v38, v38, s66, -v132
	s_waitcnt lgkmcnt(0)
	v_mfma_f32_16x16x32_bf16 v[156:159], v[168:171], v[172:175], v[156:159]
	ds_read2_b64 v[168:171], v177 offset0:64 offset1:68
	v_mul_f32_e32 v38, 0x3fb8aa3b, v38
	v_fma_f32 v42, v42, s66, -v132
	s_waitcnt lgkmcnt(0)
	v_mfma_f32_16x16x32_bf16 v[164:167], v[168:171], v[172:175], v[164:167]
	ds_read2_b64 v[168:171], v49 offset0:96 offset1:100
	v_mul_f32_e32 v42, 0x3fb8aa3b, v42
	v_fma_f32 v30, v30, s66, -v132
	s_waitcnt lgkmcnt(0)
	v_mfma_f32_16x16x32_bf16 v[148:151], v[168:171], v[172:175], v[148:151]
	v_exp_f32_e32 v173, v38
	v_fma_f32 v38, v43, s66, -v132
	v_mul_f32_e32 v38, 0x3fb8aa3b, v38
	v_exp_f32_e32 v174, v38
	v_fma_f32 v38, v39, s66, -v132
	v_mul_f32_e32 v38, 0x3fb8aa3b, v38
	v_exp_f32_e32 v175, v38
	v_fma_f32 v38, v44, s66, -v132
	v_mul_f32_e32 v38, 0x3fb8aa3b, v38
	v_exp_f32_e32 v178, v38
	v_fma_f32 v38, v40, s66, -v132
	v_mul_f32_e32 v38, 0x3fb8aa3b, v38
	v_exp_f32_e32 v172, v42
	v_exp_f32_e32 v179, v38
	v_fma_f32 v38, v45, s66, -v132
	ds_read2_b64 v[42:45], v52 offset0:8 offset1:12
	v_mul_f32_e32 v38, 0x3fb8aa3b, v38
	v_exp_f32_e32 v180, v38
	v_fma_f32 v38, v41, s66, -v132
	v_mul_f32_e32 v38, 0x3fb8aa3b, v38
	v_exp_f32_e32 v181, v38
	v_cvt_pk_bf16_f32 v38, v172, v174
	v_cvt_pk_bf16_f32 v39, v178, v180
	v_cvt_pk_bf16_f32 v40, v173, v175
	v_cvt_pk_bf16_f32 v41, v179, v181
	v_mul_f32_e32 v30, 0x3fb8aa3b, v30
	v_fma_f32 v22, v22, s66, -v132
	s_waitcnt lgkmcnt(0)
	v_mfma_f32_16x16x32_bf16 v[42:45], v[42:45], v[38:41], v[160:163]
	v_mul_f32_e32 v22, 0x3fb8aa3b, v22
	v_fma_f32 v26, v26, s66, -v132
	v_mul_f32_e32 v26, 0x3fb8aa3b, v26
	ds_read2_b64 v[160:163], v176 offset0:40 offset1:44
	s_waitcnt lgkmcnt(0)
	v_mfma_f32_16x16x32_bf16 v[156:159], v[160:163], v[38:41], v[156:159]
	ds_read2_b64 v[160:163], v177 offset0:72 offset1:76
	v_fma_f32 v2, v2, s66, -v132
	v_mul_f32_e32 v2, 0x3fb8aa3b, v2
	s_waitcnt lgkmcnt(0)
	v_mfma_f32_16x16x32_bf16 v[160:163], v[160:163], v[38:41], v[164:167]
	s_nop 2
	ds_read2_b64 v[164:167], v49 offset0:104 offset1:108
	global_load_dwordx4 v[168:171], v[6:7], off offset:384
	s_nop 0
	global_load_dwordx4 v[6:9], v[8:9], off offset:384
	s_waitcnt vmcnt(5)
	ds_write_b128 v75, v[186:189]
	s_waitcnt vmcnt(4)
	ds_write_b128 v75, v[190:193] offset:9216
	s_waitcnt lgkmcnt(2)
	v_mfma_f32_16x16x32_bf16 v[38:41], v[164:167], v[38:41], v[148:151]
	v_exp_f32_e32 v164, v30
	v_fma_f32 v30, v34, s66, -v132
	v_mul_f32_e32 v30, 0x3fb8aa3b, v30
	v_exp_f32_e32 v165, v30
	v_fma_f32 v30, v31, s66, -v132
	v_mul_f32_e32 v30, 0x3fb8aa3b, v30
	v_exp_f32_e32 v166, v30
	v_fma_f32 v30, v35, s66, -v132
	v_mul_f32_e32 v30, 0x3fb8aa3b, v30
	v_exp_f32_e32 v167, v30
	v_fma_f32 v30, v32, s66, -v132
	v_mul_f32_e32 v30, 0x3fb8aa3b, v30
	v_exp_f32_e32 v182, v30
	v_fma_f32 v30, v36, s66, -v132
	v_mul_f32_e32 v30, 0x3fb8aa3b, v30
	v_exp_f32_e32 v183, v30
	v_fma_f32 v30, v33, s66, -v132
	s_waitcnt lgkmcnt(0)
	s_barrier
	v_mul_f32_e32 v34, 0x3fb8aa3b, v30
	ds_read2_b64 v[30:33], v155 offset1:4
	v_exp_f32_e32 v184, v34
	v_fma_f32 v34, v37, s66, -v132
	v_mul_f32_e32 v34, 0x3fb8aa3b, v34
	v_exp_f32_e32 v185, v34
	v_cvt_pk_bf16_f32 v34, v164, v166
	v_cvt_pk_bf16_f32 v35, v182, v184
	v_cvt_pk_bf16_f32 v36, v165, v167
	v_cvt_pk_bf16_f32 v37, v183, v185
	ds_read2_b64 v[148:151], v152 offset0:64 offset1:68
	v_fma_f32 v10, v10, s66, -v132
	s_waitcnt lgkmcnt(1)
	v_mfma_f32_16x16x32_bf16 v[30:33], v[30:33], v[34:37], v[42:45]
	v_mul_f32_e32 v10, 0x3fb8aa3b, v10
	s_nop 1
	ds_read2_b64 v[42:45], v147 offset0:32 offset1:36
	s_waitcnt lgkmcnt(0)
	v_mfma_f32_16x16x32_bf16 v[42:45], v[42:45], v[34:37], v[156:159]
	s_nop 2
	ds_read2_b64 v[156:159], v153 offset0:96 offset1:100
	v_mfma_f32_16x16x32_bf16 v[148:151], v[148:151], v[34:37], v[160:163]
	s_waitcnt lgkmcnt(0)
	v_mfma_f32_16x16x32_bf16 v[34:37], v[156:159], v[34:37], v[38:41]
	v_exp_f32_e32 v157, v22
	v_fma_f32 v22, v27, s66, -v132
	v_mul_f32_e32 v22, 0x3fb8aa3b, v22
	v_exp_f32_e32 v158, v22
	v_fma_f32 v22, v23, s66, -v132
	v_mul_f32_e32 v22, 0x3fb8aa3b, v22
	v_exp_f32_e32 v159, v22
	v_fma_f32 v22, v28, s66, -v132
	v_mul_f32_e32 v22, 0x3fb8aa3b, v22
	v_exp_f32_e32 v160, v22
	v_fma_f32 v22, v24, s66, -v132
	v_mul_f32_e32 v22, 0x3fb8aa3b, v22
	v_exp_f32_e32 v156, v26
	v_exp_f32_e32 v161, v22
	v_fma_f32 v22, v29, s66, -v132
	ds_read2_b64 v[26:29], v155 offset0:8 offset1:12
	v_mul_f32_e32 v22, 0x3fb8aa3b, v22
	v_exp_f32_e32 v155, v22
	v_fma_f32 v22, v25, s66, -v132
	v_mul_f32_e32 v22, 0x3fb8aa3b, v22
	v_exp_f32_e32 v162, v22
	v_cvt_pk_bf16_f32 v22, v156, v158
	v_cvt_pk_bf16_f32 v23, v160, v155
	v_cvt_pk_bf16_f32 v24, v157, v159
	v_cvt_pk_bf16_f32 v25, v161, v162
	ds_read2_b64 v[38:41], v152 offset0:72 offset1:76
	s_waitcnt lgkmcnt(1)
	v_mfma_f32_16x16x32_bf16 v[26:29], v[26:29], v[22:25], v[30:33]
	s_nop 2
	ds_read2_b64 v[30:33], v147 offset0:40 offset1:44
	s_waitcnt lgkmcnt(0)
	v_mfma_f32_16x16x32_bf16 v[30:33], v[30:33], v[22:25], v[42:45]
	s_nop 2
	ds_read2_b64 v[42:45], v153 offset0:104 offset1:108
	s_waitcnt vmcnt(1)
	ds_write_b128 v75, v[168:171] offset:18432
	s_waitcnt vmcnt(0)
	ds_write_b128 v75, v[6:9] offset:27648
	v_fma_f32 v6, v14, s66, -v132
	v_mul_f32_e32 v6, 0x3fb8aa3b, v6
	v_mfma_f32_16x16x32_bf16 v[38:41], v[38:41], v[22:25], v[148:151]
	s_waitcnt lgkmcnt(0)
	s_barrier
; #define LAS __attribute__((address_space(3)))
; __device__ __forceinline__ unsigned cvt_pk_bf16(float lo, float hi) { const float __attribute__((ext_vector_type(2))) v = {lo, hi}; return __builtin_bit_cast(unsigned, __builtin_convertvector(v, bf16x2_t)); }
; template <bool LOCAL>
; __device__ __forceinline__ void na_unit(const bf16* P, const bf16* VT, bf16* YCAT, const LAS float* rpb_l, LAS bf16* buf, int b, int gr, int hp, int qblk, int tid) {
;     ...
;                 for (int e = 0; e < 4; ++e) { p[e] = __expf(sl[2 * (c < 8 ? c : 0)][e] - m); p[4 + e] = __expf(sl[2 * (c < 8 ? c : 0) + 1][e] - m); }
; #pragma unroll
;                 for (int e = 0; e < 8; ++e) lsum += p[e];
;                 const bf16x8 pf = __builtin_bit_cast(bf16x8, (v4u){pg8::cvt_pk_bf16(p[0], p[1]), pg8::cvt_pk_bf16(p[2], p[3]), pg8::cvt_pk_bf16(p[4], p[5]), pg8::cvt_pk_bf16(p[6], p[7])});
; #pragma unroll
;                 for (int dt = 0; dt < 4; ++dt) { const LAS bf16* vp = cb + (16 * dt + fr) * 72 + kc0 + 4 * fq;
;                     o[dt] = __builtin_amdgcn_mfma_f32_16x16x32_bf16(frag44(vp, vp + 16), pf, o[dt], 0, 0, 0); }
;             } else {
;                 const int cc = c - NLOC;
; #pragma unroll
;                 for (int p2 = 0; p2 < 2; ++p2) {
;                     float p[8];
; #pragma unroll
;                     for (int e = 0; e < 4; ++e) { p[e] = __expf(sc[4 * (cc >= 0 ? cc : 0) + 2 * p2][e] - m); p[4 + e] = __expf(sc[4 * (cc >= 0 ? cc : 0) + 2 * p2 + 1][e] - m); }
; #pragma unroll
;                     for (int e = 0; e < 8; ++e) lsum += p[e];
;                     const bf16x8 pf = __builtin_bit_cast(bf16x8, (v4u){pg8::cvt_pk_bf16(p[0], p[1]), pg8::cvt_pk_bf16(p[2], p[3]), pg8::cvt_pk_bf16(p[4], p[5]), pg8::cvt_pk_bf16(p[6], p[7])});
; #pragma unroll
;                     for (int dt = 0; dt < 4; ++dt) { const LAS bf16* vp = cb + (16 * dt + fr) * 72 + 32 * p2 + 4 * fq;
;                         o[dt] = __builtin_amdgcn_mfma_f32_16x16x32_bf16(frag44(vp, vp + 16), pf, o[dt], 0, 0, 0); }
;                 }
;             }
;         }
;         if (sidx + 1 < 2 * NCH) NA_STORE(sidx + 1);
;         __syncthreads();
;     }
;     ...
;     lsum += __shfl_xor(lsum, 16); lsum += __shfl_xor(lsum, 32);
;     const float inv = 1.f / lsum;
	v_mfma_f32_16x16x32_bf16 v[22:25], v[42:45], v[22:25], v[34:37]
	v_ashrrev_i32_e32 v75, 31, v74
	s_nop 1
	v_exp_f32_e32 v34, v6
	v_fma_f32 v6, v18, s66, -v132
	v_mul_f32_e32 v6, 0x3fb8aa3b, v6
	v_exp_f32_e32 v35, v6
	v_fma_f32 v6, v15, s66, -v132
	v_mul_f32_e32 v6, 0x3fb8aa3b, v6
	v_exp_f32_e32 v36, v6
	v_fma_f32 v6, v19, s66, -v132
	v_mul_f32_e32 v6, 0x3fb8aa3b, v6
	v_exp_f32_e32 v37, v6
	v_fma_f32 v6, v16, s66, -v132
	v_mul_f32_e32 v6, 0x3fb8aa3b, v6
	v_exp_f32_e32 v42, v6
	v_fma_f32 v6, v20, s66, -v132
	v_mul_f32_e32 v6, 0x3fb8aa3b, v6
	v_exp_f32_e32 v43, v6
	v_fma_f32 v6, v17, s66, -v132
	v_mul_f32_e32 v14, 0x3fb8aa3b, v6
	ds_read2_b64 v[6:9], v52 offset1:4
	v_exp_f32_e32 v44, v14
	v_fma_f32 v14, v21, s66, -v132
	v_mul_f32_e32 v14, 0x3fb8aa3b, v14
	v_exp_f32_e32 v45, v14
	v_cvt_pk_bf16_f32 v14, v34, v36
	v_cvt_pk_bf16_f32 v15, v42, v44
	v_cvt_pk_bf16_f32 v16, v35, v37
	v_cvt_pk_bf16_f32 v17, v43, v45
	ds_read2_b64 v[18:21], v176 offset0:32 offset1:36
	s_waitcnt lgkmcnt(1)
	v_mfma_f32_16x16x32_bf16 v[6:9], v[6:9], v[14:17], v[26:29]
	s_nop 2
	ds_read2_b64 v[26:29], v177 offset0:64 offset1:68
	s_waitcnt lgkmcnt(0)
	v_mfma_f32_16x16x32_bf16 v[26:29], v[26:29], v[14:17], v[38:41]
	s_nop 2
	v_add_f32_e32 v38, 0, v126
	v_add_f32_e32 v38, v95, v38
	v_add_f32_e32 v38, v94, v38
	v_add_f32_e32 v38, v99, v38
	v_add_f32_e32 v38, v91, v38
	v_add_f32_e32 v38, v90, v38
	v_add_f32_e32 v38, v93, v38
	v_add_f32_e32 v38, v92, v38
	v_add_f32_e32 v38, v85, v38
	v_add_f32_e32 v38, v89, v38
	v_add_f32_e32 v38, v97, v38
	v_add_f32_e32 v38, v98, v38
	v_add_f32_e32 v38, v76, v38
	v_add_f32_e32 v38, v86, v38
	v_add_f32_e32 v38, v96, v38
	v_add_f32_e32 v38, v100, v38
	v_add_f32_e32 v38, v103, v38
	v_add_f32_e32 v38, v104, v38
	v_add_f32_e32 v38, v107, v38
	v_add_f32_e32 v38, v106, v38
	v_add_f32_e32 v38, v101, v38
	v_add_f32_e32 v38, v102, v38
	v_add_f32_e32 v38, v105, v38
	v_add_f32_e32 v38, v108, v38
	v_add_f32_e32 v38, v110, v38
	v_add_f32_e32 v38, v112, v38
	v_add_f32_e32 v38, v114, v38
	v_add_f32_e32 v38, v115, v38
	v_add_f32_e32 v38, v109, v38
	v_add_f32_e32 v38, v111, v38
	v_add_f32_e32 v38, v113, v38
	v_add_f32_e32 v38, v116, v38
	v_add_f32_e32 v38, v118, v38
	v_add_f32_e32 v38, v120, v38
	v_add_f32_e32 v38, v122, v38
	v_add_f32_e32 v38, v123, v38
	v_add_f32_e32 v38, v117, v38
	v_add_f32_e32 v38, v119, v38
	v_add_f32_e32 v38, v121, v38
	v_add_f32_e32 v38, v124, v38
	v_add_f32_e32 v38, v127, v38
	v_add_f32_e32 v38, v129, v38
	v_add_f32_e32 v38, v131, v38
	v_add_f32_e32 v38, v133, v38
	v_add_f32_e32 v38, v125, v38
	v_add_f32_e32 v38, v128, v38
	v_add_f32_e32 v38, v130, v38
	v_add_f32_e32 v38, v134, v38
	v_add_f32_e32 v38, v136, v38
	v_add_f32_e32 v38, v138, v38
	v_add_f32_e32 v38, v140, v38
	v_add_f32_e32 v38, v141, v38
	v_add_f32_e32 v38, v135, v38
	v_add_f32_e32 v38, v137, v38
	v_add_f32_e32 v38, v139, v38
	v_add_f32_e32 v38, v142, v38
	v_add_f32_e32 v38, v78, v38
	v_add_f32_e32 v38, v80, v38
	v_add_f32_e32 v38, v143, v38
	v_add_f32_e32 v38, v145, v38
	v_add_f32_e32 v38, v70, v38
	v_add_f32_e32 v38, v79, v38
	v_add_f32_e32 v38, v81, v38
	v_add_f32_e32 v38, v144, v38
	v_add_f32_e32 v38, v146, v38
	v_add_f32_e32 v38, v66, v38
	v_add_f32_e32 v38, v67, v38
	v_add_f32_e32 v38, v68, v38
	v_add_f32_e32 v38, v62, v38
	v_add_f32_e32 v38, v63, v38
	v_add_f32_e32 v38, v64, v38
	v_add_f32_e32 v38, v65, v38
	v_add_f32_e32 v38, v58, v38
	v_add_f32_e32 v38, v59, v38
	v_add_f32_e32 v38, v60, v38
	v_add_f32_e32 v38, v61, v38
	v_add_f32_e32 v38, v54, v38
	v_add_f32_e32 v38, v55, v38
	v_add_f32_e32 v38, v56, v38
	v_add_f32_e32 v38, v57, v38
	v_add_f32_e32 v38, v69, v38
	v_add_f32_e32 v38, v50, v38
	v_add_f32_e32 v38, v51, v38
	v_add_f32_e32 v38, v154, v38
	v_add_f32_e32 v38, v46, v38
	v_add_f32_e32 v38, v47, v38
	v_add_f32_e32 v38, v48, v38
	v_add_f32_e32 v38, v53, v38
	v_add_f32_e32 v38, v172, v38
	v_mfma_f32_16x16x32_bf16 v[18:21], v[18:21], v[14:17], v[30:33]
	v_add_f32_e32 v38, v174, v38
	v_add_f32_e32 v38, v178, v38
	v_add_f32_e32 v38, v180, v38
	ds_read2_b64 v[30:33], v49 offset0:96 offset1:100
	v_add_f32_e32 v38, v173, v38
	v_add_f32_e32 v38, v175, v38
	v_add_f32_e32 v38, v179, v38
	v_add_f32_e32 v38, v181, v38
	v_add_f32_e32 v38, v164, v38
	v_add_f32_e32 v38, v166, v38
	s_waitcnt lgkmcnt(0)
	v_mfma_f32_16x16x32_bf16 v[14:17], v[30:33], v[14:17], v[22:25]
	v_add_f32_e32 v38, v182, v38
	s_nop 1
	v_exp_f32_e32 v23, v2
	v_fma_f32 v2, v11, s66, -v132
	v_mul_f32_e32 v2, 0x3fb8aa3b, v2
	v_add_f32_e32 v38, v184, v38
	v_exp_f32_e32 v24, v2
	v_fma_f32 v2, v3, s66, -v132
	v_add_f32_e32 v38, v165, v38
	v_mul_f32_e32 v2, 0x3fb8aa3b, v2
	v_add_f32_e32 v38, v167, v38
	v_exp_f32_e32 v25, v2
	v_fma_f32 v2, v12, s66, -v132
	v_add_f32_e32 v38, v183, v38
	v_mul_f32_e32 v2, 0x3fb8aa3b, v2
	v_add_f32_e32 v38, v185, v38
	v_exp_f32_e32 v30, v2
	v_fma_f32 v2, v4, s66, -v132
	v_add_f32_e32 v38, v156, v38
	v_mul_f32_e32 v2, 0x3fb8aa3b, v2
	v_add_f32_e32 v38, v158, v38
	v_exp_f32_e32 v22, v10
	v_exp_f32_e32 v31, v2
	v_fma_f32 v2, v13, s66, -v132
	ds_read2_b64 v[10:13], v52 offset0:8 offset1:12
	v_add_f32_e32 v38, v160, v38
	v_mul_f32_e32 v2, 0x3fb8aa3b, v2
	v_add_f32_e32 v38, v155, v38
	v_exp_f32_e32 v32, v2
	v_fma_f32 v2, v5, s66, -v132
	v_add_f32_e32 v38, v157, v38
	v_mul_f32_e32 v2, 0x3fb8aa3b, v2
	v_add_f32_e32 v38, v159, v38
	v_exp_f32_e32 v33, v2
	v_add_f32_e32 v38, v161, v38
	v_add_f32_e32 v38, v162, v38
	v_add_f32_e32 v34, v34, v38
	v_add_f32_e32 v34, v36, v34
	v_cvt_pk_bf16_f32 v2, v22, v24
	v_cvt_pk_bf16_f32 v3, v30, v32
	v_cvt_pk_bf16_f32 v4, v23, v25
	v_cvt_pk_bf16_f32 v5, v31, v33
	v_add_f32_e32 v34, v42, v34
	v_add_f32_e32 v34, v44, v34
	s_waitcnt lgkmcnt(0)
	v_mfma_f32_16x16x32_bf16 v[6:9], v[10:13], v[2:5], v[6:9]
	ds_read2_b64 v[10:13], v176 offset0:40 offset1:44
	v_add_f32_e32 v34, v35, v34
	v_add_f32_e32 v34, v37, v34
	v_add_f32_e32 v34, v43, v34
	v_add_f32_e32 v34, v45, v34
	v_add_f32_e32 v22, v22, v34
	v_add_f32_e32 v22, v24, v22
	v_add_f32_e32 v22, v30, v22
	v_add_f32_e32 v22, v32, v22
	s_waitcnt lgkmcnt(0)
	v_mfma_f32_16x16x32_bf16 v[10:13], v[10:13], v[2:5], v[18:21]
	v_add_f32_e32 v22, v23, v22
	v_add_f32_e32 v22, v25, v22
	v_add_f32_e32 v22, v31, v22
	ds_read2_b64 v[18:21], v177 offset0:72 offset1:76
	v_add_f32_e32 v30, v33, v22
	ds_bpermute_b32 v31, v87, v30
	ds_read2_b64 v[22:25], v49 offset0:104 offset1:108
	s_waitcnt lgkmcnt(2)
	v_mfma_f32_16x16x32_bf16 v[18:21], v[18:21], v[2:5], v[26:29]
	s_waitcnt lgkmcnt(1)
	s_nop 1
	v_add_f32_e32 v26, v30, v31
	ds_bpermute_b32 v27, v88, v26
	v_lshlrev_b32_e32 v70, 1, v77
	s_waitcnt lgkmcnt(1)
	v_mfma_f32_16x16x32_bf16 v[14:17], v[22:25], v[2:5], v[14:17]
	s_waitcnt lgkmcnt(0)
	s_barrier
; __device__ __forceinline__ unsigned cvt_pk_bf16(float lo, float hi) { const float __attribute__((ext_vector_type(2))) v = {lo, hi}; return __builtin_bit_cast(unsigned, __builtin_convertvector(v, bf16x2_t)); }
; template <bool LOCAL>
; __device__ __forceinline__ void na_unit(const bf16* P, const bf16* VT, bf16* YCAT, const LAS float* rpb_l, LAS bf16* buf, int b, int gr, int hp, int qblk, int tid) {
;     ...
;     lsum += __shfl_xor(lsum, 16); lsum += __shfl_xor(lsum, 32);
;     const float inv = 1.f / lsum;
;     bf16* op = YCAT + (size_t)(qrow0 + fr) * D + 512 + h * 64 + 4 * fq;
; #pragma unroll
;     for (int dt = 0; dt < 4; ++dt) { v2u w; w.x = pg8::cvt_pk_bf16(o[dt][0] * inv, o[dt][1] * inv); w.y = pg8::cvt_pk_bf16(o[dt][2] * inv, o[dt][3] * inv); *(v2u*)(op + dt * 16) = w; }
	v_add_f32_e32 v2, v26, v27
	v_div_scale_f32 v3, s[0:1], v2, v2, 1.0
	v_rcp_f32_e32 v4, v3
	s_nop 0
	v_fma_f32 v5, -v3, v4, 1.0
	v_fmac_f32_e32 v4, v5, v4
	v_div_scale_f32 v5, vcc, 1.0, v2, 1.0
	v_mul_f32_e32 v22, v5, v4
	v_fma_f32 v23, -v3, v22, v5
	v_fmac_f32_e32 v22, v23, v4
	v_fma_f32 v3, -v3, v22, v5
	v_div_fmas_f32 v3, v3, v4, v22
	v_div_fixup_f32 v22, v3, v2, 1.0
	v_lshlrev_b64 v[2:3], 11, v[74:75]
	v_lshl_add_u64 v[2:3], s[10:11], 0, v[2:3]
	v_lshl_add_u64 v[2:3], v[72:73], 1, v[2:3]
	v_pk_mul_f32 v[6:7], v[6:7], v[22:23] op_sel_hi:[1,0]
	v_pk_mul_f32 v[8:9], v[8:9], v[22:23] op_sel_hi:[1,0]
	v_lshl_add_u64 v[4:5], v[2:3], 0, v[70:71]
	v_cvt_pk_bf16_f32 v6, v6, v7
	v_cvt_pk_bf16_f32 v7, v8, v9
	global_store_dwordx2 v[4:5], v[6:7], off offset:1024
	v_pk_mul_f32 v[6:7], v[10:11], v[22:23] op_sel_hi:[1,0]
	v_pk_mul_f32 v[8:9], v[12:13], v[22:23] op_sel_hi:[1,0]
	v_cvt_pk_bf16_f32 v6, v6, v7
	v_cvt_pk_bf16_f32 v7, v8, v9
	global_store_dwordx2 v[4:5], v[6:7], off offset:1056
	v_pk_mul_f32 v[6:7], v[18:19], v[22:23] op_sel_hi:[1,0]
	v_pk_mul_f32 v[8:9], v[20:21], v[22:23] op_sel_hi:[1,0]
	v_cvt_pk_bf16_f32 v6, v6, v7
	v_cvt_pk_bf16_f32 v7, v8, v9
	v_lshl_add_u64 v[2:3], v[4:5], 0, s[12:13]
	global_store_dwordx2 v[4:5], v[6:7], off offset:1088
	v_pk_mul_f32 v[4:5], v[14:15], v[22:23] op_sel_hi:[1,0]
	v_pk_mul_f32 v[6:7], v[16:17], v[22:23] op_sel_hi:[1,0]
	v_cvt_pk_bf16_f32 v4, v4, v5

; __global__ void __launch_bounds__(NTHR, 2) mk_fwd(Args args) {
;     extern __shared__ __attribute__((aligned(16))) unsigned char lds[];
	.amdhsa_kernel _Z6mk_fwd4Args
		.amdhsa_group_segment_fixed_size 0
		.amdhsa_private_segment_fixed_size 0
		.amdhsa_kernarg_size 520
		.amdhsa_user_sgpr_count 2
		.amdhsa_user_sgpr_dispatch_ptr 0
		.amdhsa_user_sgpr_queue_ptr 0
		.amdhsa_user_sgpr_kernarg_segment_ptr 1
		.amdhsa_user_sgpr_dispatch_id 0
		.amdhsa_user_sgpr_kernarg_preload_length 0
		.amdhsa_user_sgpr_kernarg_preload_offset 0
		.amdhsa_user_sgpr_private_segment_size 0
		.amdhsa_uses_dynamic_stack 0
		.amdhsa_enable_private_segment 0
		.amdhsa_system_sgpr_workgroup_id_x 1
		.amdhsa_system_sgpr_workgroup_id_y 0
		.amdhsa_system_sgpr_workgroup_id_z 0
		.amdhsa_system_sgpr_workgroup_info 0
		.amdhsa_system_vgpr_workitem_id 0
		.amdhsa_next_free_vgpr 256
		.amdhsa_next_free_sgpr 102
		.amdhsa_accum_offset 256
		.amdhsa_reserve_vcc 1
		.amdhsa_float_round_mode_32 0
		.amdhsa_float_round_mode_16_64 0
		.amdhsa_float_denorm_mode_32 3
		.amdhsa_float_denorm_mode_16_64 3
		.amdhsa_dx10_clamp 1
		.amdhsa_ieee_mode 1
		.amdhsa_fp16_overflow 0
		.amdhsa_tg_split 0
		.amdhsa_exception_fp_ieee_invalid_op 0
		.amdhsa_exception_fp_denorm_src 0
		.amdhsa_exception_fp_ieee_div_zero 0
		.amdhsa_exception_fp_ieee_overflow 0
		.amdhsa_exception_fp_ieee_underflow 0
		.amdhsa_exception_fp_ieee_inexact 0
		.amdhsa_exception_int_div_zero 0
	.end_amdhsa_kernel

; __global__ void __launch_bounds__(NTHR, 2) mk_fwd(Args args) {
amdhsa.kernels:
  - .agpr_count:     0
    .args:
      - .offset:         0
        .size:           264
        .value_kind:     by_value
      - .offset:         264
        .size:           4
        .value_kind:     hidden_block_count_x
      - .offset:         268
        .size:           4
        .value_kind:     hidden_block_count_y
      - .offset:         272
        .size:           4
        .value_kind:     hidden_block_count_z
      - .offset:         276
        .size:           2
        .value_kind:     hidden_group_size_x
      - .offset:         278
        .size:           2
        .value_kind:     hidden_group_size_y
      - .offset:         280
        .size:           2
        .value_kind:     hidden_group_size_z
      - .offset:         282
        .size:           2
        .value_kind:     hidden_remainder_x
      - .offset:         284
        .size:           2
        .value_kind:     hidden_remainder_y
      - .offset:         286
        .size:           2
        .value_kind:     hidden_remainder_z
      - .offset:         304
        .size:           8
        .value_kind:     hidden_global_offset_x
      - .offset:         312
        .size:           8
        .value_kind:     hidden_global_offset_y
      - .offset:         320
        .size:           8
        .value_kind:     hidden_global_offset_z
      - .offset:         328
        .size:           2
        .value_kind:     hidden_grid_dims
      - .offset:         384
        .size:           4
        .value_kind:     hidden_dynamic_lds_size
    .group_segment_fixed_size: 0
    .kernarg_segment_align: 8
    .kernarg_segment_size: 520
    .language:       OpenCL C
    .language_version:
      - 2
      - 0
    .max_flat_workgroup_size: 512
    .name:           _Z6mk_fwd4Args
    .private_segment_fixed_size: 0
    .sgpr_count:     108
    .sgpr_spill_count: 304
    .symbol:         _Z6mk_fwd4Args.kd
    .uniform_work_group_size: 1
    .uses_dynamic_stack: false
    .vgpr_count:     256
    .vgpr_spill_count: 0
    .wavefront_size: 64
